# layer-1 w_down and w_out transpositions in the layer-1 in-projection idle slot (54 region steps per idle workgroup)
# baseline (speedup 1.0000x reference)
; #define LAS __attribute__((address_space(3)))
; #define LDS_WAIT() asm volatile("s_waitcnt lgkmcnt(0)" ::: "memory")
; #define PHASE_IDS() int tid_l_ = threadIdx.x; asm volatile("" : "+v"(tid_l_)); const int tid = tid_l_, lane = tid & 63, wave = __builtin_amdgcn_readfirstlane(tid >> 6); \
;     const int gw = F.vcu * NWAVES + wave, NGW = F.G * NWAVES, gt = F.vcu * (NWAVES * 64) + tid, NGT = F.G * NWAVES * 64; (void)gw; (void)NGW; (void)gt; (void)NGT; (void)lane
; template <int MAP, bool KS, bool KPERM = false>
; __device__ __forceinline__ void p0_transpose_item(const float* W, int K, int Nsrc, int nblk, bf16* WT, const float* ksA, const float* ksB, int ksplit, LAS float* scr, int item, int lane) {
;     ...
;     for (int i = 0; i < 32; ++i) { const int kk = 2 * i + (lane >> 5); const int k = k0 + kk;
;         if (KS) v[i] *= (k < ksplit ? ksA[k] : ksB[k - ksplit]);
;         scr[kk * 33 + (lane & 31)] = v[i]; }
;     LDS_WAIT(); asm volatile("" ::: "memory");
;     const int c = lane & 7;
; #pragma unroll
;     for (int j = 0; j < 4; ++j) { const int n = (lane >> 3) + 8 * j; const LAS float* s = scr + (8 * c) * 33 + n;
; __global__ void __launch_bounds__(NWAVES * 64, 2) hybrid_fwd(Args args) {
;     ...
;         PHASE_IDS();
;         LAS float* scr = (LAS float*)(F.lds + RING_OFF + wave * 16384);
;         constexpr int I_IN = (DM / 64) * (NPROJ / 32), I_O = (DM / 64) * (DM / 32), I_UP = (DM / 64) * (FF / 32), I_DN = (FF / 64) * (DM / 32);
;         constexpr int I_L = I_IN + I_O + I_UP + I_DN;
;         for (int rep = 0; rep < REP_PRO; ++rep)
;         for (int it = gw; it < DEPTH * I_L; it += NGW) {
.LBB0_11:
	s_or_b64 exec, exec, s[0:1]
	v_mov_b32_e32 v1, v0
	v_readlane_b32 s1, v253, 2
	v_readfirstlane_b32 s0, v1
	s_ashr_i32 s0, s0, 6
	s_lshl_b32 s1, s1, 3
	s_add_i32 s80, s0, s1
	s_lshl_b32 s0, s0, 14
	v_lshlrev_b32_e32 v2, 3, v1
	v_writelane_b32 v253, s1, 46
	s_add_i32 s1, s0, 0
	v_and_b32_e32 v18, 31, v1
	v_bfe_u32 v20, v1, 3, 3
	v_and_b32_e32 v8, 56, v2
	s_lshl_b32 s96, s83, 3
	s_lshl_b32 s76, s83, 9
	v_bfe_u32 v6, v1, 5, 1
	v_lshl_add_u32 v25, v18, 2, s1
	s_movk_i32 s0, 0x84
	v_mul_u32_u24_e32 v2, 0x84, v8
	v_lshlrev_b32_e32 v3, 2, v20
	s_cmp_gt_i32 s80, 0x2f3ff
	v_mad_u32_u24 v19, v6, s0, v25
	v_mov_b32_e32 v11, 0
	v_add3_u32 v21, s1, v2, v3
	v_or_b32_e32 v22, 8, v20
	v_or_b32_e32 v23, 16, v20
	v_or_b32_e32 v24, 24, v20
	s_cbranch_scc1 .Lco3_hop_192
	v_and_b32_e32 v249, 63, v0
	v_lshrrev_b32_e32 v250, 6, v0
	v_readlane_b32 s15, v253, 2
	s_lshr_b32 s22, s15, 3
	s_and_b32 s23, s15, 7
	v_lshrrev_b32_e32 v246, 5, v249
	v_lshl_add_u32 v247, v250, 4, v246
	v_and_b32_e32 v248, 31, v249
	v_xor_b32_e32 v248, v248, v250
	v_lshlrev_b32_e32 v248, 4, v248
	v_lshl_add_u32 v209, v247, 9, v248
	v_add_u32_e32 v210, 0x10000, v209
	v_lshlrev_b32_e32 v96, 2, v247
	v_and_b32_e32 v248, 31, v249
	v_lshlrev_b32_e32 v248, 4, v248
	s_mov_b32 s20, 0x10000
	v_mad_u32_u24 v74, v247, s20, v248
	s_mov_b32 s20, 0x4000
	v_mad_u32_u24 v75, v247, s20, v248
	s_mov_b32 s20, 0xb140
	v_mad_u32_u24 v76, v247, s20, v248
	v_and_b32_e32 v246, 7, v249
	v_lshrrev_b32_e32 v247, 5, v249
	v_lshl_add_u32 v247, v250, 2, v247
	v_xor_b32_e32 v247, v247, v246
	v_lshlrev_b32_e32 v247, 4, v247
	v_lshl_add_u32 v247, v246, 13, v247
	v_bfe_u32 v248, v249, 3, 2
	v_lshl_add_u32 v211, v248, 2, v247
	v_add_u32_e32 v212, 0x10000, v211
	v_and_b32_e32 v246, 7, v249
	v_lshrrev_b32_e32 v247, 5, v249
	v_lshl_add_u32 v247, v250, 2, v247
	v_add_u32_e32 v247, 2, v247
	v_xor_b32_e32 v247, v247, v246
	v_lshlrev_b32_e32 v247, 4, v247
	v_lshl_add_u32 v247, v246, 13, v247
	v_bfe_u32 v248, v249, 3, 2
	v_lshl_add_u32 v213, v248, 2, v247
	v_add_u32_e32 v214, 0x10000, v213
	v_and_b32_e32 v246, 15, v249
	v_lshrrev_b32_e32 v247, 1, v246
	v_lshlrev_b32_e32 v248, 2, v250
	v_xor_b32_e32 v248, v248, v247
	v_lshlrev_b32_e32 v248, 4, v248
	v_lshl_add_u32 v248, v246, 12, v248
	v_lshrrev_b32_e32 v247, 4, v249
	v_lshl_add_u32 v112, v247, 2, v248
	v_add_u32_e32 v113, 0x10000, v112
	v_and_b32_e32 v246, 15, v249
	v_lshrrev_b32_e32 v247, 1, v246
	v_lshlrev_b32_e32 v248, 2, v250
	v_add_u32_e32 v248, 1, v248
	v_xor_b32_e32 v248, v248, v247
	v_lshlrev_b32_e32 v248, 4, v248
	v_lshl_add_u32 v248, v246, 12, v248
	v_lshrrev_b32_e32 v247, 4, v249
	v_lshl_add_u32 v114, v247, 2, v248
	v_add_u32_e32 v115, 0x10000, v114
	v_and_b32_e32 v246, 15, v249
	v_lshrrev_b32_e32 v247, 1, v246
	v_lshlrev_b32_e32 v248, 2, v250
	v_add_u32_e32 v248, 2, v248
	v_xor_b32_e32 v248, v248, v247
	v_lshlrev_b32_e32 v248, 4, v248
	v_lshl_add_u32 v248, v246, 12, v248
	v_lshrrev_b32_e32 v247, 4, v249
	v_lshl_add_u32 v116, v247, 2, v248
	v_add_u32_e32 v117, 0x10000, v116
	v_and_b32_e32 v246, 15, v249
	v_lshrrev_b32_e32 v247, 1, v246
	v_lshlrev_b32_e32 v248, 2, v250
	v_add_u32_e32 v248, 3, v248
	v_xor_b32_e32 v248, v248, v247
	v_lshlrev_b32_e32 v248, 4, v248
	v_lshl_add_u32 v248, v246, 12, v248
	v_lshrrev_b32_e32 v247, 4, v249
	v_lshl_add_u32 v118, v247, 2, v248
	v_add_u32_e32 v119, 0x10000, v118
	v_lshrrev_b32_e32 v246, 3, v249
	v_lshl_add_u32 v246, v250, 4, v246
	v_and_b32_e32 v247, 7, v249
	v_lshlrev_b32_e32 v247, 4, v247
	v_lshl_add_u32 v77, v246, 12, v247
	v_lshl_add_u32 v79, v246, 14, v247
	v_and_b32_e32 v248, 63, v246
	v_lshlrev_b32_e32 v248, 1, v248
	v_lshrrev_b32_e32 v246, 6, v246
	v_or_b32_e32 v248, v248, v246
	v_lshl_add_u32 v81, v248, 12, v247
	v_lshrrev_b32_e32 v246, 3, v249
	v_lshl_add_u32 v246, v250, 4, v246
	v_add_u32_e32 v246, 8, v246
	v_and_b32_e32 v247, 7, v249
	v_lshlrev_b32_e32 v247, 4, v247
	v_lshl_add_u32 v78, v246, 12, v247
	v_lshl_add_u32 v80, v246, 14, v247
	v_and_b32_e32 v248, 63, v246
	v_lshlrev_b32_e32 v248, 1, v248
	v_lshrrev_b32_e32 v246, 6, v246
	v_or_b32_e32 v248, v248, v246
	v_lshl_add_u32 v82, v248, 12, v247
	v_lshrrev_b32_e32 v246, 4, v249
	v_lshl_add_u32 v246, v250, 4, v246
	v_and_b32_e32 v247, 15, v249
	v_lshlrev_b32_e32 v247, 4, v247
	v_lshl_add_u32 v83, v246, 13, v247
	v_and_b32_e32 v248, 63, v246
	v_lshlrev_b32_e32 v248, 1, v248
	v_lshrrev_b32_e32 v246, 6, v246
	v_or_b32_e32 v248, v248, v246
	v_lshl_add_u32 v87, v248, 13, v247
	v_lshrrev_b32_e32 v246, 4, v249
	v_lshl_add_u32 v246, v250, 4, v246
	v_add_u32_e32 v246, 4, v246
	v_and_b32_e32 v247, 15, v249
	v_lshlrev_b32_e32 v247, 4, v247
	v_lshl_add_u32 v84, v246, 13, v247
	v_and_b32_e32 v248, 63, v246
	v_lshlrev_b32_e32 v248, 1, v248
	v_lshrrev_b32_e32 v246, 6, v246
	v_or_b32_e32 v248, v248, v246
	v_lshl_add_u32 v88, v248, 13, v247
	v_lshrrev_b32_e32 v246, 4, v249
	v_lshl_add_u32 v246, v250, 4, v246
	v_add_u32_e32 v246, 8, v246
	v_and_b32_e32 v247, 15, v249
	v_lshlrev_b32_e32 v247, 4, v247
	v_lshl_add_u32 v85, v246, 13, v247
	v_and_b32_e32 v248, 63, v246
	v_lshlrev_b32_e32 v248, 1, v248
	v_lshrrev_b32_e32 v246, 6, v246
	v_or_b32_e32 v248, v248, v246
	v_lshl_add_u32 v89, v248, 13, v247
	v_lshrrev_b32_e32 v246, 4, v249
	v_lshl_add_u32 v246, v250, 4, v246
	v_add_u32_e32 v246, 12, v246
	v_and_b32_e32 v247, 15, v249
	v_lshlrev_b32_e32 v247, 4, v247
	v_lshl_add_u32 v86, v246, 13, v247
	v_and_b32_e32 v248, 63, v246
	v_lshlrev_b32_e32 v248, 1, v248
	v_lshrrev_b32_e32 v246, 6, v246
	v_or_b32_e32 v248, v248, v246
	v_lshl_add_u32 v90, v248, 13, v247
	v_mov_b32_e32 v95, 0x43e00000
	s_mov_b32 s62, 0xc3e00000
	s_mov_b32 s63, 0x7fff
	s_mov_b32 s64, 0x07060302
	v_readlane_b32 s10, v253, 5
;     ...
;     for (int i = 0; i < 32; ++i) { const int k = k0 + 2 * i + (lane >> 5); float x = v[i] * wscale; if (KS) x *= (k < ksplit ? ksA[k] : ksB[k - ksplit]); scr[(2 * i + (lane >> 5)) * 33 + (lane & 31)] = x; }
; __global__ void __launch_bounds__(NWAVES * 64, 2) hybrid_fwd(Args args) {
;     ...
;             if (r < I_IN) { if (l >= PROJ_F8_FROM) p0_transpose_item_f8<true, 1>(args.in[2] + (size_t)l * DM * NSRC, DM, NSRC, NPROJ / 32, (unsigned char*)(ws + WS_WIN + l * SZ_WIN), WUP8_SCALE, args.in[1] + l * DM, args.in[1] + l * DM, DM, scr, r, lane);
;                 else p0_transpose_item<1, true>(args.in[2] + (size_t)l * DM * NSRC, DM, NSRC, NPROJ / 32, (bf16*)(ws + WS_WIN + l * SZ_WIN), args.in[1] + l * DM, args.in[1] + l * DM, DM, scr, r, lane); continue; } r -= I_IN;
;             if (r < I_O) { if (l >= WO_F8_FROM) p0_transpose_item_f8<true>(args.in[13] + (size_t)l * DM * DM, DM, DM, DM / 32, (unsigned char*)(ws + WS_WO + l * SZ_WO), 64.f, args.in[6] + l * 2048, args.in[12] + l * 2048, 2048, scr, r, lane);
;                 else p0_transpose_item<0, true>(args.in[13] + (size_t)l * DM * DM, DM, DM, DM / 32, (bf16*)(ws + WS_WO + l * SZ_WO), args.in[6] + l * 2048, args.in[12] + l * 2048, 2048, scr, r, lane); continue; } r -= I_O;
;             if (r < I_UP) { p0_transpose_item_f8<true>(args.in[15] + (size_t)l * DM * FF, DM, FF, FF / 32, (unsigned char*)(ws + WS_WUP + l * SZ_WUP), WUP8_SCALE, args.in[14] + l * DM, args.in[14] + l * DM, DM, scr, r, lane); continue; } r -= I_UP;
	v_readlane_b32 s11, v253, 6
	s_lshl_b32 s20, s22, 9
	s_add_u32 s10, s10, s20
	s_addc_u32 s11, s11, 0
	global_load_dword v42, v96, s[10:11] offset:0
	global_load_dword v43, v96, s[10:11] offset:8
	global_load_dword v44, v96, s[10:11] offset:16
	global_load_dword v45, v96, s[10:11] offset:24
	global_load_dword v46, v96, s[10:11] offset:32
	global_load_dword v47, v96, s[10:11] offset:40
	global_load_dword v48, v96, s[10:11] offset:48
	global_load_dword v49, v96, s[10:11] offset:56
	v_readlane_b32 s10, v253, 5
	v_readlane_b32 s11, v253, 6
	s_lshl_b32 s20, s22, 9
	s_add_i32 s20, s20, 0x4000
	s_add_u32 s10, s10, s20
	s_addc_u32 s11, s11, 0
	global_load_dword v50, v96, s[10:11] offset:0
	global_load_dword v51, v96, s[10:11] offset:8
	global_load_dword v52, v96, s[10:11] offset:16
	global_load_dword v53, v96, s[10:11] offset:24
	global_load_dword v54, v96, s[10:11] offset:32
	global_load_dword v55, v96, s[10:11] offset:40
	global_load_dword v56, v96, s[10:11] offset:48
	global_load_dword v57, v96, s[10:11] offset:56
	v_readlane_b32 s10, v253, 15
	v_readlane_b32 s11, v253, 16
	v_readlane_b32 s20, v253, 27
	v_readlane_b32 s21, v253, 28
	s_sub_i32 s26, s22, 16
	s_cmp_lt_u32 s22, 16
	s_cselect_b32 s10, s10, s20
	s_cselect_b32 s11, s11, s21
	s_cselect_b32 s26, s22, s26
	s_lshl_b32 s20, s26, 9
	s_add_u32 s10, s10, s20
	s_addc_u32 s11, s11, 0
	global_load_dword v58, v96, s[10:11] offset:0
	global_load_dword v59, v96, s[10:11] offset:8
	global_load_dword v60, v96, s[10:11] offset:16
	global_load_dword v61, v96, s[10:11] offset:24
	global_load_dword v62, v96, s[10:11] offset:32
	global_load_dword v63, v96, s[10:11] offset:40
	global_load_dword v64, v96, s[10:11] offset:48
	global_load_dword v65, v96, s[10:11] offset:56
	v_readlane_b32 s10, v253, 15
	v_readlane_b32 s11, v253, 16
	v_readlane_b32 s20, v253, 27
	v_readlane_b32 s21, v253, 28
	s_sub_i32 s26, s22, 16
	s_cmp_lt_u32 s22, 16
	s_cselect_b32 s10, s10, s20
	s_cselect_b32 s11, s11, s21
	s_cselect_b32 s26, s22, s26
	s_lshl_b32 s20, s26, 9
	s_add_i32 s20, s20, 0x2000
	s_add_u32 s10, s10, s20
	s_addc_u32 s11, s11, 0
	global_load_dword v66, v96, s[10:11] offset:0
	global_load_dword v67, v96, s[10:11] offset:8
	global_load_dword v68, v96, s[10:11] offset:16
	global_load_dword v69, v96, s[10:11] offset:24
	global_load_dword v70, v96, s[10:11] offset:32
	global_load_dword v71, v96, s[10:11] offset:40
	global_load_dword v72, v96, s[10:11] offset:48
	global_load_dword v73, v96, s[10:11] offset:56
	v_readlane_b32 s10, v253, 31
	v_readlane_b32 s11, v253, 32
	s_lshl_b32 s20, s22, 9
	s_add_u32 s10, s10, s20
	s_addc_u32 s11, s11, 0
	global_load_dword v26, v96, s[10:11] offset:0
	global_load_dword v27, v96, s[10:11] offset:8
	global_load_dword v28, v96, s[10:11] offset:16
	global_load_dword v29, v96, s[10:11] offset:24
	global_load_dword v30, v96, s[10:11] offset:32
	global_load_dword v31, v96, s[10:11] offset:40
	global_load_dword v32, v96, s[10:11] offset:48
	global_load_dword v33, v96, s[10:11] offset:56
	v_readlane_b32 s10, v253, 31
	v_readlane_b32 s11, v253, 32
	s_lshl_b32 s20, s22, 9
	s_add_i32 s20, s20, 0x4000
	s_add_u32 s10, s10, s20
	s_addc_u32 s11, s11, 0
	global_load_dword v34, v96, s[10:11] offset:0
	global_load_dword v35, v96, s[10:11] offset:8
	global_load_dword v36, v96, s[10:11] offset:16
	global_load_dword v37, v96, s[10:11] offset:24
	global_load_dword v38, v96, s[10:11] offset:32
	global_load_dword v39, v96, s[10:11] offset:40
	global_load_dword v40, v96, s[10:11] offset:48
	global_load_dword v41, v96, s[10:11] offset:56
	s_waitcnt vmcnt(0)
	v_mul_f32_e32 v50, 0x42800000, v50
	v_mul_f32_e32 v51, 0x42800000, v51
	v_mul_f32_e32 v52, 0x42800000, v52
	v_mul_f32_e32 v53, 0x42800000, v53
	v_mul_f32_e32 v54, 0x42800000, v54
	v_mul_f32_e32 v55, 0x42800000, v55
	v_mul_f32_e32 v56, 0x42800000, v56
	v_mul_f32_e32 v57, 0x42800000, v57
	v_mul_f32_e32 v66, 0x42800000, v66
	v_mul_f32_e32 v67, 0x42800000, v67
	v_mul_f32_e32 v68, 0x42800000, v68
	v_mul_f32_e32 v69, 0x42800000, v69
	v_mul_f32_e32 v70, 0x42800000, v70
	v_mul_f32_e32 v71, 0x42800000, v71
	v_mul_f32_e32 v72, 0x42800000, v72
	v_mul_f32_e32 v73, 0x42800000, v73
	v_mul_f32_e32 v26, 0x42800000, v26
	v_mul_f32_e32 v27, 0x42800000, v27
	v_mul_f32_e32 v28, 0x42800000, v28
	v_mul_f32_e32 v29, 0x42800000, v29
	v_mul_f32_e32 v30, 0x42800000, v30
	v_mul_f32_e32 v31, 0x42800000, v31
	v_mul_f32_e32 v32, 0x42800000, v32
	v_mul_f32_e32 v33, 0x42800000, v33
	v_mul_f32_e32 v34, 0x42800000, v34
	v_mul_f32_e32 v35, 0x42800000, v35
	v_mul_f32_e32 v36, 0x42800000, v36
	v_mul_f32_e32 v37, 0x42800000, v37
	v_mul_f32_e32 v38, 0x42800000, v38
	v_mul_f32_e32 v39, 0x42800000, v39
	v_mul_f32_e32 v40, 0x42800000, v40
	v_mul_f32_e32 v41, 0x42800000, v41
	v_readlane_b32 s30, v253, 33
	v_readlane_b32 s31, v253, 34
	v_readlane_b32 s32, v253, 41
	v_readlane_b32 s33, v253, 42
	s_mul_i32 s20, s22, 0x800000
	s_lshl_b32 s21, s23, 9
	s_add_u32 s20, s20, s21
	s_add_u32 s30, s30, s20
	s_addc_u32 s31, s31, 0
	s_add_u32 s32, s32, 0xf600000
	s_addc_u32 s33, s33, 0
	s_lshl_b32 s20, s22, 7
	s_mul_i32 s21, s23, 0x80000
	s_add_u32 s20, s20, s21
	s_add_u32 s32, s32, s20
	s_addc_u32 s33, s33, 0
	v_readlane_b32 s34, v253, 33
	v_readlane_b32 s35, v253, 34
	v_readlane_b32 s36, v253, 41
	v_readlane_b32 s37, v253, 42
	s_add_u32 s34, s34, 0x10000000
	s_addc_u32 s35, s35, 0
	s_mul_i32 s20, s22, 0x800000
	s_lshl_b32 s21, s23, 9
	s_add_u32 s20, s20, s21
	s_add_u32 s34, s34, s20
	s_addc_u32 s35, s35, 0
	s_add_u32 s36, s36, 0x17600000
	s_addc_u32 s37, s37, 0
	s_lshl_b32 s20, s22, 7
	s_mul_i32 s21, s23, 0x80000
	s_add_u32 s20, s20, s21
	s_add_u32 s36, s36, s20
	s_addc_u32 s37, s37, 0
	v_readlane_b32 s38, v253, 35
;     const int pr = item >> 1, kb = 2 * (pr / nblk) + (item & 1), nb = pr % nblk, k0 = 64 * kb, n0 = 32 * nb;
;     const int nr = n0 + (lane & 31); const int sc = MAP == 1 ? src_col_in(nr) : nr;
;     float v[32];
; #pragma unroll
;     for (int i = 0; i < 32; ++i) v[i] = sc >= 0 ? W[(size_t)(k0 + 2 * i + (lane >> 5)) * Nsrc + sc] : 0.f;
; #pragma unroll
;     for (int i = 0; i < 32; ++i) { const int k = k0 + 2 * i + (lane >> 5); float x = v[i] * wscale; if (KS) x *= (k < ksplit ? ksA[k] : ksB[k - ksplit]); scr[(2 * i + (lane >> 5)) * 33 + (lane & 31)] = x; }
; __global__ void __launch_bounds__(NWAVES * 64, 2) hybrid_fwd(Args args) {
;     ...
;             if (r < I_IN) { if (l >= PROJ_F8_FROM) p0_transpose_item_f8<true, 1>(args.in[2] + (size_t)l * DM * NSRC, DM, NSRC, NPROJ / 32, (unsigned char*)(ws + WS_WIN + l * SZ_WIN), WUP8_SCALE, args.in[1] + l * DM, args.in[1] + l * DM, DM, scr, r, lane);
;                 else p0_transpose_item<1, true>(args.in[2] + (size_t)l * DM * NSRC, DM, NSRC, NPROJ / 32, (bf16*)(ws + WS_WIN + l * SZ_WIN), args.in[1] + l * DM, args.in[1] + l * DM, DM, scr, r, lane); continue; } r -= I_IN;
;             if (r < I_O) { if (l >= WO_F8_FROM) p0_transpose_item_f8<true>(args.in[13] + (size_t)l * DM * DM, DM, DM, DM / 32, (unsigned char*)(ws + WS_WO + l * SZ_WO), 64.f, args.in[6] + l * 2048, args.in[12] + l * 2048, 2048, scr, r, lane);
;                 else p0_transpose_item<0, true>(args.in[13] + (size_t)l * DM * DM, DM, DM, DM / 32, (bf16*)(ws + WS_WO + l * SZ_WO), args.in[6] + l * 2048, args.in[12] + l * 2048, 2048, scr, r, lane); continue; } r -= I_O;
;             if (r < I_UP) { p0_transpose_item_f8<true>(args.in[15] + (size_t)l * DM * FF, DM, FF, FF / 32, (unsigned char*)(ws + WS_WUP + l * SZ_WUP), WUP8_SCALE, args.in[14] + l * DM, args.in[14] + l * DM, DM, scr, r, lane); continue; } r -= I_UP;
;             p0_transpose_item_f8<false>(args.in[16] + (size_t)l * FF * DM, FF, DM, DM / 32, (unsigned char*)(ws + WS_WDN + l * SZ_WDN), 128.f, args.in[16], args.in[16], 0, scr, r, lane);
	v_readlane_b32 s39, v253, 36
	v_readlane_b32 s40, v253, 41
	v_readlane_b32 s41, v253, 42
	s_mul_i32 s20, s22, 0x200000
	s_lshl_b32 s21, s23, 9
	s_add_u32 s20, s20, s21
	s_add_u32 s38, s38, s20
	s_addc_u32 s39, s39, 0
	s_add_u32 s40, s40, 0x1f600000
	s_addc_u32 s41, s41, 0
	s_lshl_b32 s20, s22, 7
	s_mul_i32 s21, s23, 0x200000
	s_add_u32 s20, s20, s21
	s_add_u32 s40, s40, s20
	s_addc_u32 s41, s41, 0
	v_readlane_b32 s42, v253, 35
	v_readlane_b32 s43, v253, 36
	v_readlane_b32 s44, v253, 41
	v_readlane_b32 s45, v253, 42
	s_add_u32 s42, s42, 0x10000000
	s_addc_u32 s43, s43, 0
	s_mul_i32 s20, s22, 0x200000
	s_lshl_b32 s21, s23, 9
	s_add_u32 s20, s20, s21
	s_add_u32 s42, s42, s20
	s_addc_u32 s43, s43, 0
	s_add_u32 s44, s44, 0x27600000
	s_addc_u32 s45, s45, 0
	s_lshl_b32 s20, s22, 7
	s_mul_i32 s21, s23, 0x200000
	s_add_u32 s20, s20, s21
	s_add_u32 s44, s44, s20
	s_addc_u32 s45, s45, 0
	v_readlane_b32 s46, v253, 7
	v_readlane_b32 s47, v253, 8
	v_readlane_b32 s48, v253, 41
	v_readlane_b32 s49, v253, 42
	s_mul_i32 s20, s22, 0x58a000
	s_add_u32 s46, s46, s20
	s_addc_u32 s47, s47, 0
	s_add_u32 s48, s48, 0x200000
	s_addc_u32 s49, s49, 0
	s_lshl_b32 s20, s22, 8
	s_add_u32 s48, s48, s20
	s_addc_u32 s49, s49, 0
	v_readlane_b32 s50, v253, 7
	v_readlane_b32 s51, v253, 8
	v_readlane_b32 s52, v253, 41
	v_readlane_b32 s53, v253, 42
	s_add_u32 s50, s50, 0xb140000
	s_addc_u32 s51, s51, 0
	s_mul_i32 s20, s22, 0x58a000
	s_add_u32 s50, s50, s20
	s_addc_u32 s51, s51, 0
	s_add_u32 s52, s52, 0x5c00000
	s_addc_u32 s53, s53, 0
	s_lshl_b32 s20, s22, 7
	s_add_u32 s52, s52, s20
	s_addc_u32 s53, s53, 0
	v_readlane_b32 s54, v253, 29
	v_readlane_b32 s55, v253, 30
	v_readlane_b32 s56, v253, 41
	v_readlane_b32 s57, v253, 42
	s_mul_i32 s20, s22, 0x200000
	s_lshl_b32 s21, s23, 9
	s_add_u32 s20, s20, s21
	s_add_u32 s54, s54, s20
	s_addc_u32 s55, s55, 0
	s_add_u32 s56, s56, 0xb600000
	s_addc_u32 s57, s57, 0
	s_lshl_b32 s20, s22, 8
	s_mul_i32 s21, s23, 0x100000
	s_add_u32 s20, s20, s21
	s_add_u32 s56, s56, s20
	s_addc_u32 s57, s57, 0
	v_readlane_b32 s58, v253, 29
	v_readlane_b32 s59, v253, 30
	v_readlane_b32 s60, v253, 41
	v_readlane_b32 s61, v253, 42
	s_add_u32 s58, s58, 0x4000000
	s_addc_u32 s59, s59, 0
	s_mul_i32 s20, s22, 0x200000
	s_lshl_b32 s21, s23, 9
	s_add_u32 s20, s20, s21
	s_add_u32 s58, s58, s20
	s_addc_u32 s59, s59, 0
	s_add_u32 s60, s60, 0xd600000
	s_addc_u32 s61, s61, 0
	s_lshl_b32 s20, s22, 7
	s_mul_i32 s21, s23, 0x80000
	s_add_u32 s20, s20, s21
	s_add_u32 s60, s60, s20
	s_addc_u32 s61, s61, 0
	s_mov_b64 s[8:9], s[30:31]
	global_load_dwordx4 v[144:147], v74, s[8:9]
	s_add_u32 s8, s8, 0x20000
	s_addc_u32 s9, s9, 0
	global_load_dwordx4 v[148:151], v74, s[8:9]
	s_add_u32 s8, s8, 0x20000
	s_addc_u32 s9, s9, 0
	global_load_dwordx4 v[152:155], v74, s[8:9]
	s_add_u32 s8, s8, 0x20000
	s_addc_u32 s9, s9, 0
	global_load_dwordx4 v[156:159], v74, s[8:9]
	s_add_u32 s8, s8, 0x20000
	s_addc_u32 s9, s9, 0
	global_load_dwordx4 v[160:163], v74, s[8:9]
	s_add_u32 s8, s8, 0x20000
	s_addc_u32 s9, s9, 0
	global_load_dwordx4 v[164:167], v74, s[8:9]
	s_add_u32 s8, s8, 0x20000
	s_addc_u32 s9, s9, 0
	global_load_dwordx4 v[168:171], v74, s[8:9]
	s_add_u32 s8, s8, 0x20000
	s_addc_u32 s9, s9, 0
	global_load_dwordx4 v[172:175], v74, s[8:9]
	s_add_u32 s8, s30, 0x1000
	s_addc_u32 s9, s31, 0
	global_load_dwordx4 v[176:179], v74, s[8:9]
	s_add_u32 s8, s8, 0x20000
	s_addc_u32 s9, s9, 0
	global_load_dwordx4 v[180:183], v74, s[8:9]
	s_add_u32 s8, s8, 0x20000
	s_addc_u32 s9, s9, 0
	global_load_dwordx4 v[184:187], v74, s[8:9]
	s_add_u32 s8, s8, 0x20000
	s_addc_u32 s9, s9, 0
	global_load_dwordx4 v[188:191], v74, s[8:9]
	s_add_u32 s8, s8, 0x20000
	s_addc_u32 s9, s9, 0
	global_load_dwordx4 v[192:195], v74, s[8:9]
	s_add_u32 s8, s8, 0x20000
	s_addc_u32 s9, s9, 0
	global_load_dwordx4 v[196:199], v74, s[8:9]
	s_add_u32 s8, s8, 0x20000
	s_addc_u32 s9, s9, 0
	global_load_dwordx4 v[200:203], v74, s[8:9]
	s_add_u32 s8, s8, 0x20000
	s_addc_u32 s9, s9, 0
	global_load_dwordx4 v[204:207], v74, s[8:9]
	s_waitcnt vmcnt(8)
	v_mul_f32_e32 v144, v26, v144
	v_mul_f32_e32 v145, v26, v145
	v_mul_f32_e32 v146, v26, v146
	v_mul_f32_e32 v147, v26, v147
	ds_write_b128 v209, v[144:147]
	v_mul_f32_e32 v148, v27, v148
	v_mul_f32_e32 v149, v27, v149
	v_mul_f32_e32 v150, v27, v150
	v_mul_f32_e32 v151, v27, v151
	ds_write_b128 v209, v[148:151] offset:1024
	v_mul_f32_e32 v152, v28, v152
	v_mul_f32_e32 v153, v28, v153
	v_mul_f32_e32 v154, v28, v154
	v_mul_f32_e32 v155, v28, v155
	ds_write_b128 v209, v[152:155] offset:2048
	v_mul_f32_e32 v156, v29, v156
	v_mul_f32_e32 v157, v29, v157
	v_mul_f32_e32 v158, v29, v158
	v_mul_f32_e32 v159, v29, v159
	ds_write_b128 v209, v[156:159] offset:3072
	v_mul_f32_e32 v160, v30, v160
	v_mul_f32_e32 v161, v30, v161
	v_mul_f32_e32 v162, v30, v162
	v_mul_f32_e32 v163, v30, v163
	ds_write_b128 v209, v[160:163] offset:4096
	v_mul_f32_e32 v164, v31, v164
	v_mul_f32_e32 v165, v31, v165
	v_mul_f32_e32 v166, v31, v166
	v_mul_f32_e32 v167, v31, v167
	ds_write_b128 v209, v[164:167] offset:5120
	v_mul_f32_e32 v168, v32, v168
	v_mul_f32_e32 v169, v32, v169
	v_mul_f32_e32 v170, v32, v170
	v_mul_f32_e32 v171, v32, v171
	ds_write_b128 v209, v[168:171] offset:6144
	v_mul_f32_e32 v172, v33, v172
	v_mul_f32_e32 v173, v33, v173
	v_mul_f32_e32 v174, v33, v174
	v_mul_f32_e32 v175, v33, v175
	ds_write_b128 v209, v[172:175] offset:7168
	s_waitcnt lgkmcnt(0)
	s_barrier
; #define GAS __attribute__((address_space(1)))
; #define LAS __attribute__((address_space(3)))
; #define LDS_WAIT() asm volatile("s_waitcnt lgkmcnt(0)" ::: "memory")
; __device__ __forceinline__ unsigned pk4_fp8(float a, float b, float c, float d) {
;     a = fminf(fmaxf(a, -448.f), 448.f); b = fminf(fmaxf(b, -448.f), 448.f); c = fminf(fmaxf(c, -448.f), 448.f); d = fminf(fmaxf(d, -448.f), 448.f);
;     int w = __builtin_amdgcn_cvt_pk_fp8_f32(a, b, 0, false); w = __builtin_amdgcn_cvt_pk_fp8_f32(c, d, w, true); return (unsigned)w; }
;     const int pr = item >> 1, kb = 2 * (pr / nblk) + (item & 1), nb = pr % nblk, k0 = 64 * kb, n0 = 32 * nb;
;     const int nr = n0 + (lane & 31); const int sc = MAP == 1 ? src_col_in(nr) : nr;
;     float v[32];
; #pragma unroll
;     for (int i = 0; i < 32; ++i) v[i] = sc >= 0 ? W[(size_t)(k0 + 2 * i + (lane >> 5)) * Nsrc + sc] : 0.f;
; #pragma unroll
;     for (int i = 0; i < 32; ++i) { const int k = k0 + 2 * i + (lane >> 5); float x = v[i] * wscale; if (KS) x *= (k < ksplit ? ksA[k] : ksB[k - ksplit]); scr[(2 * i + (lane >> 5)) * 33 + (lane & 31)] = x; }
;     LDS_WAIT(); asm volatile("" ::: "memory");
;     const int c = lane & 7;
; #pragma unroll
;     for (int j = 0; j < 4; ++j) { const int n = (lane >> 3) + 8 * j; const LAS float* s = scr + (8 * c) * 33 + n;
;         const unsigned long long o = (unsigned long long)pg8::pk4_fp8(s[0 * 33], s[1 * 33], s[2 * 33], s[3 * 33]) | ((unsigned long long)pg8::pk4_fp8(s[4 * 33], s[5 * 33], s[6 * 33], s[7 * 33]) << 32);
;         *(GAS unsigned long long*)(WT + (size_t)(n0 + n) * K + k0 + 8 * c) = o; }
;     LDS_WAIT(); asm volatile("" ::: "memory");
	s_add_u32 s8, s30, 0x2000
	s_addc_u32 s9, s31, 0
	global_load_dwordx4 v[144:147], v74, s[8:9]
	s_add_u32 s8, s8, 0x20000
	s_addc_u32 s9, s9, 0
	global_load_dwordx4 v[148:151], v74, s[8:9]
	s_add_u32 s8, s8, 0x20000
	s_addc_u32 s9, s9, 0
	global_load_dwordx4 v[152:155], v74, s[8:9]
	s_add_u32 s8, s8, 0x20000
	s_addc_u32 s9, s9, 0
	global_load_dwordx4 v[156:159], v74, s[8:9]
	s_add_u32 s8, s8, 0x20000
	s_addc_u32 s9, s9, 0
	global_load_dwordx4 v[160:163], v74, s[8:9]
	s_add_u32 s8, s8, 0x20000
	s_addc_u32 s9, s9, 0
	global_load_dwordx4 v[164:167], v74, s[8:9]
	s_add_u32 s8, s8, 0x20000
	s_addc_u32 s9, s9, 0
	global_load_dwordx4 v[168:171], v74, s[8:9]
	s_add_u32 s8, s8, 0x20000
	s_addc_u32 s9, s9, 0
	global_load_dwordx4 v[172:175], v74, s[8:9]
	s_mov_b64 s[6:7], s[32:33]
	ds_read_b32 v226, v211
	ds_read_b32 v227, v211 offset:512
	ds_read_b32 v228, v211 offset:1024
	ds_read_b32 v229, v211 offset:1536
	ds_read_b32 v230, v211 offset:2048
	ds_read_b32 v231, v211 offset:2560
	ds_read_b32 v232, v211 offset:3072
	ds_read_b32 v233, v211 offset:3584
	ds_read_b32 v234, v211 offset:4096
	ds_read_b32 v235, v211 offset:4608
	ds_read_b32 v236, v211 offset:5120
	ds_read_b32 v237, v211 offset:5632
	ds_read_b32 v238, v211 offset:6144
	ds_read_b32 v239, v211 offset:6656
	ds_read_b32 v240, v211 offset:7168
	ds_read_b32 v241, v211 offset:7680
	s_waitcnt lgkmcnt(0)
	v_max_f32_e32 v226, v226, v226
	v_max_f32_e32 v227, v227, v227
	v_max_f32_e32 v228, v228, v228
	v_max_f32_e32 v229, v229, v229
	v_max_f32_e32 v230, v230, v230
	v_max_f32_e32 v231, v231, v231
	v_max_f32_e32 v232, v232, v232
	v_max_f32_e32 v233, v233, v233
	v_max_f32_e32 v234, v234, v234
	v_max_f32_e32 v235, v235, v235
	v_max_f32_e32 v236, v236, v236
	v_max_f32_e32 v237, v237, v237
	v_max_f32_e32 v238, v238, v238
	v_max_f32_e32 v239, v239, v239
	v_max_f32_e32 v240, v240, v240
	v_max_f32_e32 v241, v241, v241
	v_med3_f32 v226, v226, s62, v95
	v_med3_f32 v227, v227, s62, v95
	v_med3_f32 v228, v228, s62, v95
	v_med3_f32 v229, v229, s62, v95
	v_med3_f32 v230, v230, s62, v95
	v_med3_f32 v231, v231, s62, v95
	v_med3_f32 v232, v232, s62, v95
	v_med3_f32 v233, v233, s62, v95
	v_med3_f32 v234, v234, s62, v95
	v_med3_f32 v235, v235, s62, v95
	v_med3_f32 v236, v236, s62, v95
	v_med3_f32 v237, v237, s62, v95
	v_med3_f32 v238, v238, s62, v95
	v_med3_f32 v239, v239, s62, v95
	v_med3_f32 v240, v240, s62, v95
	v_med3_f32 v241, v241, s62, v95
	v_mov_b32_e32 v242, 0
	v_mov_b32_e32 v243, 0
	v_mov_b32_e32 v244, 0
	v_mov_b32_e32 v245, 0
	v_cvt_pk_fp8_f32 v242, v226, v227
	v_cvt_pk_fp8_f32 v243, v230, v231
	v_cvt_pk_fp8_f32 v244, v234, v235
	v_cvt_pk_fp8_f32 v245, v238, v239
	v_cvt_pk_fp8_f32 v242, v228, v229 op_sel:[0,0,1]
	v_cvt_pk_fp8_f32 v243, v232, v233 op_sel:[0,0,1]
	v_cvt_pk_fp8_f32 v244, v236, v237 op_sel:[0,0,1]
	v_cvt_pk_fp8_f32 v245, v240, v241 op_sel:[0,0,1]
	s_nop 0
	global_store_dwordx4 v77, v[242:245], s[6:7]
	ds_read_b32 v226, v213
	ds_read_b32 v227, v213 offset:512
	ds_read_b32 v228, v213 offset:1024
	ds_read_b32 v229, v213 offset:1536
	ds_read_b32 v230, v213 offset:2048
	ds_read_b32 v231, v213 offset:2560
	ds_read_b32 v232, v213 offset:3072
	ds_read_b32 v233, v213 offset:3584
	ds_read_b32 v234, v213 offset:4096
	ds_read_b32 v235, v213 offset:4608
	ds_read_b32 v236, v213 offset:5120
	ds_read_b32 v237, v213 offset:5632
	ds_read_b32 v238, v213 offset:6144
	ds_read_b32 v239, v213 offset:6656
	ds_read_b32 v240, v213 offset:7168
	ds_read_b32 v241, v213 offset:7680
	s_waitcnt lgkmcnt(0)
	v_max_f32_e32 v226, v226, v226
	v_max_f32_e32 v227, v227, v227
	v_max_f32_e32 v228, v228, v228
	v_max_f32_e32 v229, v229, v229
	v_max_f32_e32 v230, v230, v230
	v_max_f32_e32 v231, v231, v231
	v_max_f32_e32 v232, v232, v232
	v_max_f32_e32 v233, v233, v233
	v_max_f32_e32 v234, v234, v234
	v_max_f32_e32 v235, v235, v235
	v_max_f32_e32 v236, v236, v236
	v_max_f32_e32 v237, v237, v237
	v_max_f32_e32 v238, v238, v238
	v_max_f32_e32 v239, v239, v239
	v_max_f32_e32 v240, v240, v240
	v_max_f32_e32 v241, v241, v241
	v_med3_f32 v226, v226, s62, v95
	v_med3_f32 v227, v227, s62, v95
	v_med3_f32 v228, v228, s62, v95
	v_med3_f32 v229, v229, s62, v95
	v_med3_f32 v230, v230, s62, v95
	v_med3_f32 v231, v231, s62, v95
	v_med3_f32 v232, v232, s62, v95
	v_med3_f32 v233, v233, s62, v95
	v_med3_f32 v234, v234, s62, v95
	v_med3_f32 v235, v235, s62, v95
	v_med3_f32 v236, v236, s62, v95
	v_med3_f32 v237, v237, s62, v95
	v_med3_f32 v238, v238, s62, v95
	v_med3_f32 v239, v239, s62, v95
	v_med3_f32 v240, v240, s62, v95
	v_med3_f32 v241, v241, s62, v95
	v_mov_b32_e32 v242, 0
	v_mov_b32_e32 v243, 0
	v_mov_b32_e32 v244, 0
	v_mov_b32_e32 v245, 0
	v_cvt_pk_fp8_f32 v242, v226, v227
	v_cvt_pk_fp8_f32 v243, v230, v231
	v_cvt_pk_fp8_f32 v244, v234, v235
	v_cvt_pk_fp8_f32 v245, v238, v239
	v_cvt_pk_fp8_f32 v242, v228, v229 op_sel:[0,0,1]
	v_cvt_pk_fp8_f32 v243, v232, v233 op_sel:[0,0,1]
	v_cvt_pk_fp8_f32 v244, v236, v237 op_sel:[0,0,1]
	v_cvt_pk_fp8_f32 v245, v240, v241 op_sel:[0,0,1]
	s_nop 0
	global_store_dwordx4 v78, v[242:245], s[6:7]
	s_waitcnt vmcnt(10)
	v_mul_f32_e32 v176, v26, v176
	v_mul_f32_e32 v177, v26, v177
	v_mul_f32_e32 v178, v26, v178
	v_mul_f32_e32 v179, v26, v179
	ds_write_b128 v210, v[176:179]
	v_mul_f32_e32 v180, v27, v180
	v_mul_f32_e32 v181, v27, v181
	v_mul_f32_e32 v182, v27, v182
	v_mul_f32_e32 v183, v27, v183
	ds_write_b128 v210, v[180:183] offset:1024
	v_mul_f32_e32 v184, v28, v184
	v_mul_f32_e32 v185, v28, v185
	v_mul_f32_e32 v186, v28, v186
	v_mul_f32_e32 v187, v28, v187
	ds_write_b128 v210, v[184:187] offset:2048
	v_mul_f32_e32 v188, v29, v188
	v_mul_f32_e32 v189, v29, v189
	v_mul_f32_e32 v190, v29, v190
	v_mul_f32_e32 v191, v29, v191
	ds_write_b128 v210, v[188:191] offset:3072
	v_mul_f32_e32 v192, v30, v192
	v_mul_f32_e32 v193, v30, v193
	v_mul_f32_e32 v194, v30, v194
	v_mul_f32_e32 v195, v30, v195
	ds_write_b128 v210, v[192:195] offset:4096
	v_mul_f32_e32 v196, v31, v196
	v_mul_f32_e32 v197, v31, v197
	v_mul_f32_e32 v198, v31, v198
	v_mul_f32_e32 v199, v31, v199
	ds_write_b128 v210, v[196:199] offset:5120
	v_mul_f32_e32 v200, v32, v200
	v_mul_f32_e32 v201, v32, v201
	v_mul_f32_e32 v202, v32, v202
	v_mul_f32_e32 v203, v32, v203
	ds_write_b128 v210, v[200:203] offset:6144
	v_mul_f32_e32 v204, v33, v204
	v_mul_f32_e32 v205, v33, v205
	v_mul_f32_e32 v206, v33, v206
	v_mul_f32_e32 v207, v33, v207
	ds_write_b128 v210, v[204:207] offset:7168
	s_waitcnt lgkmcnt(0)
	s_barrier
; #define GAS __attribute__((address_space(1)))
; #define LAS __attribute__((address_space(3)))
; #define LDS_WAIT() asm volatile("s_waitcnt lgkmcnt(0)" ::: "memory")
; __device__ __forceinline__ unsigned pk4_fp8(float a, float b, float c, float d) {
;     a = fminf(fmaxf(a, -448.f), 448.f); b = fminf(fmaxf(b, -448.f), 448.f); c = fminf(fmaxf(c, -448.f), 448.f); d = fminf(fmaxf(d, -448.f), 448.f);
;     int w = __builtin_amdgcn_cvt_pk_fp8_f32(a, b, 0, false); w = __builtin_amdgcn_cvt_pk_fp8_f32(c, d, w, true); return (unsigned)w; }
;     const int pr = item >> 1, kb = 2 * (pr / nblk) + (item & 1), nb = pr % nblk, k0 = 64 * kb, n0 = 32 * nb;
;     const int nr = n0 + (lane & 31); const int sc = MAP == 1 ? src_col_in(nr) : nr;
;     float v[32];
; #pragma unroll
;     for (int i = 0; i < 32; ++i) v[i] = sc >= 0 ? W[(size_t)(k0 + 2 * i + (lane >> 5)) * Nsrc + sc] : 0.f;
; #pragma unroll
;     for (int i = 0; i < 32; ++i) { const int k = k0 + 2 * i + (lane >> 5); float x = v[i] * wscale; if (KS) x *= (k < ksplit ? ksA[k] : ksB[k - ksplit]); scr[(2 * i + (lane >> 5)) * 33 + (lane & 31)] = x; }
;     LDS_WAIT(); asm volatile("" ::: "memory");
;     const int c = lane & 7;
; #pragma unroll
;     for (int j = 0; j < 4; ++j) { const int n = (lane >> 3) + 8 * j; const LAS float* s = scr + (8 * c) * 33 + n;
;         const unsigned long long o = (unsigned long long)pg8::pk4_fp8(s[0 * 33], s[1 * 33], s[2 * 33], s[3 * 33]) | ((unsigned long long)pg8::pk4_fp8(s[4 * 33], s[5 * 33], s[6 * 33], s[7 * 33]) << 32);
;         *(GAS unsigned long long*)(WT + (size_t)(n0 + n) * K + k0 + 8 * c) = o; }
;     LDS_WAIT(); asm volatile("" ::: "memory");
	s_add_u32 s8, s30, 0x3000
	s_addc_u32 s9, s31, 0
	global_load_dwordx4 v[176:179], v74, s[8:9]
	s_add_u32 s8, s8, 0x20000
	s_addc_u32 s9, s9, 0
	global_load_dwordx4 v[180:183], v74, s[8:9]
	s_add_u32 s8, s8, 0x20000
	s_addc_u32 s9, s9, 0
	global_load_dwordx4 v[184:187], v74, s[8:9]
	s_add_u32 s8, s8, 0x20000
	s_addc_u32 s9, s9, 0
	global_load_dwordx4 v[188:191], v74, s[8:9]
	s_add_u32 s8, s8, 0x20000
	s_addc_u32 s9, s9, 0
	global_load_dwordx4 v[192:195], v74, s[8:9]
	s_add_u32 s8, s8, 0x20000
	s_addc_u32 s9, s9, 0
	global_load_dwordx4 v[196:199], v74, s[8:9]
	s_add_u32 s8, s8, 0x20000
	s_addc_u32 s9, s9, 0
	global_load_dwordx4 v[200:203], v74, s[8:9]
	s_add_u32 s8, s8, 0x20000
	s_addc_u32 s9, s9, 0
	global_load_dwordx4 v[204:207], v74, s[8:9]
	s_add_u32 s6, s32, 0x400000
	s_addc_u32 s7, s33, 0
	ds_read_b32 v226, v212
	ds_read_b32 v227, v212 offset:512
	ds_read_b32 v228, v212 offset:1024
	ds_read_b32 v229, v212 offset:1536
	ds_read_b32 v230, v212 offset:2048
	ds_read_b32 v231, v212 offset:2560
	ds_read_b32 v232, v212 offset:3072
	ds_read_b32 v233, v212 offset:3584
	ds_read_b32 v234, v212 offset:4096
	ds_read_b32 v235, v212 offset:4608
	ds_read_b32 v236, v212 offset:5120
	ds_read_b32 v237, v212 offset:5632
	ds_read_b32 v238, v212 offset:6144
	ds_read_b32 v239, v212 offset:6656
	ds_read_b32 v240, v212 offset:7168
	ds_read_b32 v241, v212 offset:7680
	s_waitcnt lgkmcnt(0)
	v_max_f32_e32 v226, v226, v226
	v_max_f32_e32 v227, v227, v227
	v_max_f32_e32 v228, v228, v228
	v_max_f32_e32 v229, v229, v229
	v_max_f32_e32 v230, v230, v230
	v_max_f32_e32 v231, v231, v231
	v_max_f32_e32 v232, v232, v232
	v_max_f32_e32 v233, v233, v233
	v_max_f32_e32 v234, v234, v234
	v_max_f32_e32 v235, v235, v235
	v_max_f32_e32 v236, v236, v236
	v_max_f32_e32 v237, v237, v237
	v_max_f32_e32 v238, v238, v238
	v_max_f32_e32 v239, v239, v239
	v_max_f32_e32 v240, v240, v240
	v_max_f32_e32 v241, v241, v241
	v_med3_f32 v226, v226, s62, v95
	v_med3_f32 v227, v227, s62, v95
	v_med3_f32 v228, v228, s62, v95
	v_med3_f32 v229, v229, s62, v95
	v_med3_f32 v230, v230, s62, v95
	v_med3_f32 v231, v231, s62, v95
	v_med3_f32 v232, v232, s62, v95
	v_med3_f32 v233, v233, s62, v95
	v_med3_f32 v234, v234, s62, v95
	v_med3_f32 v235, v235, s62, v95
	v_med3_f32 v236, v236, s62, v95
	v_med3_f32 v237, v237, s62, v95
	v_med3_f32 v238, v238, s62, v95
	v_med3_f32 v239, v239, s62, v95
	v_med3_f32 v240, v240, s62, v95
	v_med3_f32 v241, v241, s62, v95
	v_mov_b32_e32 v242, 0
	v_mov_b32_e32 v243, 0
	v_mov_b32_e32 v244, 0
	v_mov_b32_e32 v245, 0
	v_cvt_pk_fp8_f32 v242, v226, v227
	v_cvt_pk_fp8_f32 v243, v230, v231
	v_cvt_pk_fp8_f32 v244, v234, v235
	v_cvt_pk_fp8_f32 v245, v238, v239
	v_cvt_pk_fp8_f32 v242, v228, v229 op_sel:[0,0,1]
	v_cvt_pk_fp8_f32 v243, v232, v233 op_sel:[0,0,1]
	v_cvt_pk_fp8_f32 v244, v236, v237 op_sel:[0,0,1]
	v_cvt_pk_fp8_f32 v245, v240, v241 op_sel:[0,0,1]
	s_nop 0
	global_store_dwordx4 v77, v[242:245], s[6:7]
	ds_read_b32 v226, v214
	ds_read_b32 v227, v214 offset:512
	ds_read_b32 v228, v214 offset:1024
	ds_read_b32 v229, v214 offset:1536
	ds_read_b32 v230, v214 offset:2048
	ds_read_b32 v231, v214 offset:2560
	ds_read_b32 v232, v214 offset:3072
	ds_read_b32 v233, v214 offset:3584
	ds_read_b32 v234, v214 offset:4096
	ds_read_b32 v235, v214 offset:4608
	ds_read_b32 v236, v214 offset:5120
	ds_read_b32 v237, v214 offset:5632
	ds_read_b32 v238, v214 offset:6144
	ds_read_b32 v239, v214 offset:6656
	ds_read_b32 v240, v214 offset:7168
	ds_read_b32 v241, v214 offset:7680
	s_waitcnt lgkmcnt(0)
	v_max_f32_e32 v226, v226, v226
	v_max_f32_e32 v227, v227, v227
	v_max_f32_e32 v228, v228, v228
	v_max_f32_e32 v229, v229, v229
	v_max_f32_e32 v230, v230, v230
	v_max_f32_e32 v231, v231, v231
	v_max_f32_e32 v232, v232, v232
	v_max_f32_e32 v233, v233, v233
	v_max_f32_e32 v234, v234, v234
	v_max_f32_e32 v235, v235, v235
	v_max_f32_e32 v236, v236, v236
	v_max_f32_e32 v237, v237, v237
	v_max_f32_e32 v238, v238, v238
	v_max_f32_e32 v239, v239, v239
	v_max_f32_e32 v240, v240, v240
	v_max_f32_e32 v241, v241, v241
	v_med3_f32 v226, v226, s62, v95
	v_med3_f32 v227, v227, s62, v95
	v_med3_f32 v228, v228, s62, v95
	v_med3_f32 v229, v229, s62, v95
	v_med3_f32 v230, v230, s62, v95
	v_med3_f32 v231, v231, s62, v95
	v_med3_f32 v232, v232, s62, v95
	v_med3_f32 v233, v233, s62, v95
	v_med3_f32 v234, v234, s62, v95
	v_med3_f32 v235, v235, s62, v95
	v_med3_f32 v236, v236, s62, v95
	v_med3_f32 v237, v237, s62, v95
	v_med3_f32 v238, v238, s62, v95
	v_med3_f32 v239, v239, s62, v95
	v_med3_f32 v240, v240, s62, v95
	v_med3_f32 v241, v241, s62, v95
	v_mov_b32_e32 v242, 0
	v_mov_b32_e32 v243, 0
	v_mov_b32_e32 v244, 0
	v_mov_b32_e32 v245, 0
	v_cvt_pk_fp8_f32 v242, v226, v227
	v_cvt_pk_fp8_f32 v243, v230, v231
	v_cvt_pk_fp8_f32 v244, v234, v235
	v_cvt_pk_fp8_f32 v245, v238, v239
	v_cvt_pk_fp8_f32 v242, v228, v229 op_sel:[0,0,1]
	v_cvt_pk_fp8_f32 v243, v232, v233 op_sel:[0,0,1]
	v_cvt_pk_fp8_f32 v244, v236, v237 op_sel:[0,0,1]
	v_cvt_pk_fp8_f32 v245, v240, v241 op_sel:[0,0,1]
	s_nop 0
	global_store_dwordx4 v78, v[242:245], s[6:7]
	s_waitcnt vmcnt(12)
	v_mul_f32_e32 v144, v26, v144
	v_mul_f32_e32 v145, v26, v145
	v_mul_f32_e32 v146, v26, v146
	v_mul_f32_e32 v147, v26, v147
	ds_write_b128 v209, v[144:147]
	v_mul_f32_e32 v148, v27, v148
	v_mul_f32_e32 v149, v27, v149
	v_mul_f32_e32 v150, v27, v150
	v_mul_f32_e32 v151, v27, v151
	ds_write_b128 v209, v[148:151] offset:1024
	v_mul_f32_e32 v152, v28, v152
	v_mul_f32_e32 v153, v28, v153
	v_mul_f32_e32 v154, v28, v154
	v_mul_f32_e32 v155, v28, v155
	ds_write_b128 v209, v[152:155] offset:2048
	v_mul_f32_e32 v156, v29, v156
	v_mul_f32_e32 v157, v29, v157
	v_mul_f32_e32 v158, v29, v158
	v_mul_f32_e32 v159, v29, v159
	ds_write_b128 v209, v[156:159] offset:3072
	v_mul_f32_e32 v160, v30, v160
	v_mul_f32_e32 v161, v30, v161
	v_mul_f32_e32 v162, v30, v162
	v_mul_f32_e32 v163, v30, v163
	ds_write_b128 v209, v[160:163] offset:4096
	v_mul_f32_e32 v164, v31, v164
	v_mul_f32_e32 v165, v31, v165
	v_mul_f32_e32 v166, v31, v166
	v_mul_f32_e32 v167, v31, v167
	ds_write_b128 v209, v[164:167] offset:5120
	v_mul_f32_e32 v168, v32, v168
	v_mul_f32_e32 v169, v32, v169
	v_mul_f32_e32 v170, v32, v170
	v_mul_f32_e32 v171, v32, v171
	ds_write_b128 v209, v[168:171] offset:6144
	v_mul_f32_e32 v172, v33, v172
	v_mul_f32_e32 v173, v33, v173
	v_mul_f32_e32 v174, v33, v174
	v_mul_f32_e32 v175, v33, v175
	ds_write_b128 v209, v[172:175] offset:7168
	s_waitcnt lgkmcnt(0)
	s_barrier
; #define GAS __attribute__((address_space(1)))
; #define LAS __attribute__((address_space(3)))
; #define LDS_WAIT() asm volatile("s_waitcnt lgkmcnt(0)" ::: "memory")
; __device__ __forceinline__ unsigned pk4_fp8(float a, float b, float c, float d) {
;     a = fminf(fmaxf(a, -448.f), 448.f); b = fminf(fmaxf(b, -448.f), 448.f); c = fminf(fmaxf(c, -448.f), 448.f); d = fminf(fmaxf(d, -448.f), 448.f);
;     int w = __builtin_amdgcn_cvt_pk_fp8_f32(a, b, 0, false); w = __builtin_amdgcn_cvt_pk_fp8_f32(c, d, w, true); return (unsigned)w; }
;     const int pr = item >> 1, kb = 2 * (pr / nblk) + (item & 1), nb = pr % nblk, k0 = 64 * kb, n0 = 32 * nb;
;     const int nr = n0 + (lane & 31); const int sc = MAP == 1 ? src_col_in(nr) : nr;
;     float v[32];
; #pragma unroll
;     for (int i = 0; i < 32; ++i) v[i] = sc >= 0 ? W[(size_t)(k0 + 2 * i + (lane >> 5)) * Nsrc + sc] : 0.f;
; #pragma unroll
;     for (int i = 0; i < 32; ++i) { const int k = k0 + 2 * i + (lane >> 5); float x = v[i] * wscale; if (KS) x *= (k < ksplit ? ksA[k] : ksB[k - ksplit]); scr[(2 * i + (lane >> 5)) * 33 + (lane & 31)] = x; }
;     LDS_WAIT(); asm volatile("" ::: "memory");
;     const int c = lane & 7;
; #pragma unroll
;     for (int j = 0; j < 4; ++j) { const int n = (lane >> 3) + 8 * j; const LAS float* s = scr + (8 * c) * 33 + n;
;         const unsigned long long o = (unsigned long long)pg8::pk4_fp8(s[0 * 33], s[1 * 33], s[2 * 33], s[3 * 33]) | ((unsigned long long)pg8::pk4_fp8(s[4 * 33], s[5 * 33], s[6 * 33], s[7 * 33]) << 32);
;         *(GAS unsigned long long*)(WT + (size_t)(n0 + n) * K + k0 + 8 * c) = o; }
;     LDS_WAIT(); asm volatile("" ::: "memory");
	s_add_u32 s8, s30, 0x4000
	s_addc_u32 s9, s31, 0
	global_load_dwordx4 v[144:147], v74, s[8:9]
	s_add_u32 s8, s8, 0x20000
	s_addc_u32 s9, s9, 0
	global_load_dwordx4 v[148:151], v74, s[8:9]
	s_add_u32 s8, s8, 0x20000
	s_addc_u32 s9, s9, 0
	global_load_dwordx4 v[152:155], v74, s[8:9]
	s_add_u32 s8, s8, 0x20000
	s_addc_u32 s9, s9, 0
	global_load_dwordx4 v[156:159], v74, s[8:9]
	s_add_u32 s8, s8, 0x20000
	s_addc_u32 s9, s9, 0
	global_load_dwordx4 v[160:163], v74, s[8:9]
	s_add_u32 s8, s8, 0x20000
	s_addc_u32 s9, s9, 0
	global_load_dwordx4 v[164:167], v74, s[8:9]
	s_add_u32 s8, s8, 0x20000
	s_addc_u32 s9, s9, 0
	global_load_dwordx4 v[168:171], v74, s[8:9]
	s_add_u32 s8, s8, 0x20000
	s_addc_u32 s9, s9, 0
	global_load_dwordx4 v[172:175], v74, s[8:9]
	s_add_u32 s6, s32, 0x800000
	s_addc_u32 s7, s33, 0
	ds_read_b32 v226, v211
	ds_read_b32 v227, v211 offset:512
	ds_read_b32 v228, v211 offset:1024
	ds_read_b32 v229, v211 offset:1536
	ds_read_b32 v230, v211 offset:2048
	ds_read_b32 v231, v211 offset:2560
	ds_read_b32 v232, v211 offset:3072
	ds_read_b32 v233, v211 offset:3584
	ds_read_b32 v234, v211 offset:4096
	ds_read_b32 v235, v211 offset:4608
	ds_read_b32 v236, v211 offset:5120
	ds_read_b32 v237, v211 offset:5632
	ds_read_b32 v238, v211 offset:6144
	ds_read_b32 v239, v211 offset:6656
	ds_read_b32 v240, v211 offset:7168
	ds_read_b32 v241, v211 offset:7680
	s_waitcnt lgkmcnt(0)
	v_max_f32_e32 v226, v226, v226
	v_max_f32_e32 v227, v227, v227
	v_max_f32_e32 v228, v228, v228
	v_max_f32_e32 v229, v229, v229
	v_max_f32_e32 v230, v230, v230
	v_max_f32_e32 v231, v231, v231
	v_max_f32_e32 v232, v232, v232
	v_max_f32_e32 v233, v233, v233
	v_max_f32_e32 v234, v234, v234
	v_max_f32_e32 v235, v235, v235
	v_max_f32_e32 v236, v236, v236
	v_max_f32_e32 v237, v237, v237
	v_max_f32_e32 v238, v238, v238
	v_max_f32_e32 v239, v239, v239
	v_max_f32_e32 v240, v240, v240
	v_max_f32_e32 v241, v241, v241
	v_med3_f32 v226, v226, s62, v95
	v_med3_f32 v227, v227, s62, v95
	v_med3_f32 v228, v228, s62, v95
	v_med3_f32 v229, v229, s62, v95
	v_med3_f32 v230, v230, s62, v95
	v_med3_f32 v231, v231, s62, v95
	v_med3_f32 v232, v232, s62, v95
	v_med3_f32 v233, v233, s62, v95
	v_med3_f32 v234, v234, s62, v95
	v_med3_f32 v235, v235, s62, v95
	v_med3_f32 v236, v236, s62, v95
	v_med3_f32 v237, v237, s62, v95
	v_med3_f32 v238, v238, s62, v95
	v_med3_f32 v239, v239, s62, v95
	v_med3_f32 v240, v240, s62, v95
	v_med3_f32 v241, v241, s62, v95
	v_mov_b32_e32 v242, 0
	v_mov_b32_e32 v243, 0
	v_mov_b32_e32 v244, 0
	v_mov_b32_e32 v245, 0
	v_cvt_pk_fp8_f32 v242, v226, v227
	v_cvt_pk_fp8_f32 v243, v230, v231
	v_cvt_pk_fp8_f32 v244, v234, v235
	v_cvt_pk_fp8_f32 v245, v238, v239
	v_cvt_pk_fp8_f32 v242, v228, v229 op_sel:[0,0,1]
	v_cvt_pk_fp8_f32 v243, v232, v233 op_sel:[0,0,1]
	v_cvt_pk_fp8_f32 v244, v236, v237 op_sel:[0,0,1]
	v_cvt_pk_fp8_f32 v245, v240, v241 op_sel:[0,0,1]
	s_nop 0
	global_store_dwordx4 v77, v[242:245], s[6:7]
	ds_read_b32 v226, v213
	ds_read_b32 v227, v213 offset:512
	ds_read_b32 v228, v213 offset:1024
	ds_read_b32 v229, v213 offset:1536
	ds_read_b32 v230, v213 offset:2048
	ds_read_b32 v231, v213 offset:2560
	ds_read_b32 v232, v213 offset:3072
	ds_read_b32 v233, v213 offset:3584
	ds_read_b32 v234, v213 offset:4096
	ds_read_b32 v235, v213 offset:4608
	ds_read_b32 v236, v213 offset:5120
	ds_read_b32 v237, v213 offset:5632
	ds_read_b32 v238, v213 offset:6144
	ds_read_b32 v239, v213 offset:6656
	ds_read_b32 v240, v213 offset:7168
	ds_read_b32 v241, v213 offset:7680
	s_waitcnt lgkmcnt(0)
	v_max_f32_e32 v226, v226, v226
	v_max_f32_e32 v227, v227, v227
	v_max_f32_e32 v228, v228, v228
	v_max_f32_e32 v229, v229, v229
	v_max_f32_e32 v230, v230, v230
	v_max_f32_e32 v231, v231, v231
	v_max_f32_e32 v232, v232, v232
	v_max_f32_e32 v233, v233, v233
	v_max_f32_e32 v234, v234, v234
	v_max_f32_e32 v235, v235, v235
	v_max_f32_e32 v236, v236, v236
	v_max_f32_e32 v237, v237, v237
	v_max_f32_e32 v238, v238, v238
	v_max_f32_e32 v239, v239, v239
	v_max_f32_e32 v240, v240, v240
	v_max_f32_e32 v241, v241, v241
	v_med3_f32 v226, v226, s62, v95
	v_med3_f32 v227, v227, s62, v95
	v_med3_f32 v228, v228, s62, v95
	v_med3_f32 v229, v229, s62, v95
	v_med3_f32 v230, v230, s62, v95
	v_med3_f32 v231, v231, s62, v95
	v_med3_f32 v232, v232, s62, v95
	v_med3_f32 v233, v233, s62, v95
	v_med3_f32 v234, v234, s62, v95
	v_med3_f32 v235, v235, s62, v95
	v_med3_f32 v236, v236, s62, v95
	v_med3_f32 v237, v237, s62, v95
	v_med3_f32 v238, v238, s62, v95
	v_med3_f32 v239, v239, s62, v95
	v_med3_f32 v240, v240, s62, v95
	v_med3_f32 v241, v241, s62, v95
	v_mov_b32_e32 v242, 0
	v_mov_b32_e32 v243, 0
	v_mov_b32_e32 v244, 0
	v_mov_b32_e32 v245, 0
	v_cvt_pk_fp8_f32 v242, v226, v227
	v_cvt_pk_fp8_f32 v243, v230, v231
	v_cvt_pk_fp8_f32 v244, v234, v235
	v_cvt_pk_fp8_f32 v245, v238, v239
	v_cvt_pk_fp8_f32 v242, v228, v229 op_sel:[0,0,1]
	v_cvt_pk_fp8_f32 v243, v232, v233 op_sel:[0,0,1]
	v_cvt_pk_fp8_f32 v244, v236, v237 op_sel:[0,0,1]
	v_cvt_pk_fp8_f32 v245, v240, v241 op_sel:[0,0,1]
	s_nop 0
	global_store_dwordx4 v78, v[242:245], s[6:7]
	s_waitcnt vmcnt(12)
	v_mul_f32_e32 v176, v26, v176
	v_mul_f32_e32 v177, v26, v177
	v_mul_f32_e32 v178, v26, v178
	v_mul_f32_e32 v179, v26, v179
	ds_write_b128 v210, v[176:179]
	v_mul_f32_e32 v180, v27, v180
	v_mul_f32_e32 v181, v27, v181
	v_mul_f32_e32 v182, v27, v182
	v_mul_f32_e32 v183, v27, v183
	ds_write_b128 v210, v[180:183] offset:1024
	v_mul_f32_e32 v184, v28, v184
	v_mul_f32_e32 v185, v28, v185
	v_mul_f32_e32 v186, v28, v186
	v_mul_f32_e32 v187, v28, v187
	ds_write_b128 v210, v[184:187] offset:2048
	v_mul_f32_e32 v188, v29, v188
	v_mul_f32_e32 v189, v29, v189
	v_mul_f32_e32 v190, v29, v190
	v_mul_f32_e32 v191, v29, v191
	ds_write_b128 v210, v[188:191] offset:3072
	v_mul_f32_e32 v192, v30, v192
	v_mul_f32_e32 v193, v30, v193
	v_mul_f32_e32 v194, v30, v194
	v_mul_f32_e32 v195, v30, v195
	ds_write_b128 v210, v[192:195] offset:4096
	v_mul_f32_e32 v196, v31, v196
	v_mul_f32_e32 v197, v31, v197
	v_mul_f32_e32 v198, v31, v198
	v_mul_f32_e32 v199, v31, v199
	ds_write_b128 v210, v[196:199] offset:5120
	v_mul_f32_e32 v200, v32, v200
	v_mul_f32_e32 v201, v32, v201
	v_mul_f32_e32 v202, v32, v202
	v_mul_f32_e32 v203, v32, v203
	ds_write_b128 v210, v[200:203] offset:6144
	v_mul_f32_e32 v204, v33, v204
	v_mul_f32_e32 v205, v33, v205
	v_mul_f32_e32 v206, v33, v206
	v_mul_f32_e32 v207, v33, v207
	ds_write_b128 v210, v[204:207] offset:7168
	s_waitcnt lgkmcnt(0)
	s_barrier
; #define GAS __attribute__((address_space(1)))
; #define LAS __attribute__((address_space(3)))
; #define LDS_WAIT() asm volatile("s_waitcnt lgkmcnt(0)" ::: "memory")
; __device__ __forceinline__ unsigned pk4_fp8(float a, float b, float c, float d) {
;     a = fminf(fmaxf(a, -448.f), 448.f); b = fminf(fmaxf(b, -448.f), 448.f); c = fminf(fmaxf(c, -448.f), 448.f); d = fminf(fmaxf(d, -448.f), 448.f);
;     int w = __builtin_amdgcn_cvt_pk_fp8_f32(a, b, 0, false); w = __builtin_amdgcn_cvt_pk_fp8_f32(c, d, w, true); return (unsigned)w; }
;     const int pr = item >> 1, kb = 2 * (pr / nblk) + (item & 1), nb = pr % nblk, k0 = 64 * kb, n0 = 32 * nb;
;     const int nr = n0 + (lane & 31); const int sc = MAP == 1 ? src_col_in(nr) : nr;
;     float v[32];
; #pragma unroll
;     for (int i = 0; i < 32; ++i) v[i] = sc >= 0 ? W[(size_t)(k0 + 2 * i + (lane >> 5)) * Nsrc + sc] : 0.f;
; #pragma unroll
;     for (int i = 0; i < 32; ++i) { const int k = k0 + 2 * i + (lane >> 5); float x = v[i] * wscale; if (KS) x *= (k < ksplit ? ksA[k] : ksB[k - ksplit]); scr[(2 * i + (lane >> 5)) * 33 + (lane & 31)] = x; }
;     LDS_WAIT(); asm volatile("" ::: "memory");
;     const int c = lane & 7;
; #pragma unroll
;     for (int j = 0; j < 4; ++j) { const int n = (lane >> 3) + 8 * j; const LAS float* s = scr + (8 * c) * 33 + n;
;         const unsigned long long o = (unsigned long long)pg8::pk4_fp8(s[0 * 33], s[1 * 33], s[2 * 33], s[3 * 33]) | ((unsigned long long)pg8::pk4_fp8(s[4 * 33], s[5 * 33], s[6 * 33], s[7 * 33]) << 32);
;         *(GAS unsigned long long*)(WT + (size_t)(n0 + n) * K + k0 + 8 * c) = o; }
;     LDS_WAIT(); asm volatile("" ::: "memory");
	s_add_u32 s8, s30, 0x5000
	s_addc_u32 s9, s31, 0
	global_load_dwordx4 v[176:179], v74, s[8:9]
	s_add_u32 s8, s8, 0x20000
	s_addc_u32 s9, s9, 0
	global_load_dwordx4 v[180:183], v74, s[8:9]
	s_add_u32 s8, s8, 0x20000
	s_addc_u32 s9, s9, 0
	global_load_dwordx4 v[184:187], v74, s[8:9]
	s_add_u32 s8, s8, 0x20000
	s_addc_u32 s9, s9, 0
	global_load_dwordx4 v[188:191], v74, s[8:9]
	s_add_u32 s8, s8, 0x20000
	s_addc_u32 s9, s9, 0
	global_load_dwordx4 v[192:195], v74, s[8:9]
	s_add_u32 s8, s8, 0x20000
	s_addc_u32 s9, s9, 0
	global_load_dwordx4 v[196:199], v74, s[8:9]
	s_add_u32 s8, s8, 0x20000
	s_addc_u32 s9, s9, 0
	global_load_dwordx4 v[200:203], v74, s[8:9]
	s_add_u32 s8, s8, 0x20000
	s_addc_u32 s9, s9, 0
	global_load_dwordx4 v[204:207], v74, s[8:9]
	s_add_u32 s6, s32, 0xc00000
	s_addc_u32 s7, s33, 0
	ds_read_b32 v226, v212
	ds_read_b32 v227, v212 offset:512
	ds_read_b32 v228, v212 offset:1024
	ds_read_b32 v229, v212 offset:1536
	ds_read_b32 v230, v212 offset:2048
	ds_read_b32 v231, v212 offset:2560
	ds_read_b32 v232, v212 offset:3072
	ds_read_b32 v233, v212 offset:3584
	ds_read_b32 v234, v212 offset:4096
	ds_read_b32 v235, v212 offset:4608
	ds_read_b32 v236, v212 offset:5120
	ds_read_b32 v237, v212 offset:5632
	ds_read_b32 v238, v212 offset:6144
	ds_read_b32 v239, v212 offset:6656
	ds_read_b32 v240, v212 offset:7168
	ds_read_b32 v241, v212 offset:7680
	s_waitcnt lgkmcnt(0)
	v_max_f32_e32 v226, v226, v226
	v_max_f32_e32 v227, v227, v227
	v_max_f32_e32 v228, v228, v228
	v_max_f32_e32 v229, v229, v229
	v_max_f32_e32 v230, v230, v230
	v_max_f32_e32 v231, v231, v231
	v_max_f32_e32 v232, v232, v232
	v_max_f32_e32 v233, v233, v233
	v_max_f32_e32 v234, v234, v234
	v_max_f32_e32 v235, v235, v235
	v_max_f32_e32 v236, v236, v236
	v_max_f32_e32 v237, v237, v237
	v_max_f32_e32 v238, v238, v238
	v_max_f32_e32 v239, v239, v239
	v_max_f32_e32 v240, v240, v240
	v_max_f32_e32 v241, v241, v241
	v_med3_f32 v226, v226, s62, v95
	v_med3_f32 v227, v227, s62, v95
	v_med3_f32 v228, v228, s62, v95
	v_med3_f32 v229, v229, s62, v95
	v_med3_f32 v230, v230, s62, v95
	v_med3_f32 v231, v231, s62, v95
	v_med3_f32 v232, v232, s62, v95
	v_med3_f32 v233, v233, s62, v95
	v_med3_f32 v234, v234, s62, v95
	v_med3_f32 v235, v235, s62, v95
	v_med3_f32 v236, v236, s62, v95
	v_med3_f32 v237, v237, s62, v95
	v_med3_f32 v238, v238, s62, v95
	v_med3_f32 v239, v239, s62, v95
	v_med3_f32 v240, v240, s62, v95
	v_med3_f32 v241, v241, s62, v95
	v_mov_b32_e32 v242, 0
	v_mov_b32_e32 v243, 0
	v_mov_b32_e32 v244, 0
	v_mov_b32_e32 v245, 0
	v_cvt_pk_fp8_f32 v242, v226, v227
	v_cvt_pk_fp8_f32 v243, v230, v231
	v_cvt_pk_fp8_f32 v244, v234, v235
	v_cvt_pk_fp8_f32 v245, v238, v239
	v_cvt_pk_fp8_f32 v242, v228, v229 op_sel:[0,0,1]
	v_cvt_pk_fp8_f32 v243, v232, v233 op_sel:[0,0,1]
	v_cvt_pk_fp8_f32 v244, v236, v237 op_sel:[0,0,1]
	v_cvt_pk_fp8_f32 v245, v240, v241 op_sel:[0,0,1]
	s_nop 0
	global_store_dwordx4 v77, v[242:245], s[6:7]
	ds_read_b32 v226, v214
	ds_read_b32 v227, v214 offset:512
	ds_read_b32 v228, v214 offset:1024
	ds_read_b32 v229, v214 offset:1536
	ds_read_b32 v230, v214 offset:2048
	ds_read_b32 v231, v214 offset:2560
	ds_read_b32 v232, v214 offset:3072
	ds_read_b32 v233, v214 offset:3584
	ds_read_b32 v234, v214 offset:4096
	ds_read_b32 v235, v214 offset:4608
	ds_read_b32 v236, v214 offset:5120
	ds_read_b32 v237, v214 offset:5632
	ds_read_b32 v238, v214 offset:6144
	ds_read_b32 v239, v214 offset:6656
	ds_read_b32 v240, v214 offset:7168
	ds_read_b32 v241, v214 offset:7680
	s_waitcnt lgkmcnt(0)
	v_max_f32_e32 v226, v226, v226
	v_max_f32_e32 v227, v227, v227
	v_max_f32_e32 v228, v228, v228
	v_max_f32_e32 v229, v229, v229
	v_max_f32_e32 v230, v230, v230
	v_max_f32_e32 v231, v231, v231
	v_max_f32_e32 v232, v232, v232
	v_max_f32_e32 v233, v233, v233
	v_max_f32_e32 v234, v234, v234
	v_max_f32_e32 v235, v235, v235
	v_max_f32_e32 v236, v236, v236
	v_max_f32_e32 v237, v237, v237
	v_max_f32_e32 v238, v238, v238
	v_max_f32_e32 v239, v239, v239
	v_max_f32_e32 v240, v240, v240
	v_max_f32_e32 v241, v241, v241
	v_med3_f32 v226, v226, s62, v95
	v_med3_f32 v227, v227, s62, v95
	v_med3_f32 v228, v228, s62, v95
	v_med3_f32 v229, v229, s62, v95
	v_med3_f32 v230, v230, s62, v95
	v_med3_f32 v231, v231, s62, v95
	v_med3_f32 v232, v232, s62, v95
	v_med3_f32 v233, v233, s62, v95
	v_med3_f32 v234, v234, s62, v95
	v_med3_f32 v235, v235, s62, v95
	v_med3_f32 v236, v236, s62, v95
	v_med3_f32 v237, v237, s62, v95
	v_med3_f32 v238, v238, s62, v95
	v_med3_f32 v239, v239, s62, v95
	v_med3_f32 v240, v240, s62, v95
	v_med3_f32 v241, v241, s62, v95
	v_mov_b32_e32 v242, 0
	v_mov_b32_e32 v243, 0
	v_mov_b32_e32 v244, 0
	v_mov_b32_e32 v245, 0
	v_cvt_pk_fp8_f32 v242, v226, v227
	v_cvt_pk_fp8_f32 v243, v230, v231
	v_cvt_pk_fp8_f32 v244, v234, v235
	v_cvt_pk_fp8_f32 v245, v238, v239
	v_cvt_pk_fp8_f32 v242, v228, v229 op_sel:[0,0,1]
	v_cvt_pk_fp8_f32 v243, v232, v233 op_sel:[0,0,1]
	v_cvt_pk_fp8_f32 v244, v236, v237 op_sel:[0,0,1]
	v_cvt_pk_fp8_f32 v245, v240, v241 op_sel:[0,0,1]
	s_nop 0
	global_store_dwordx4 v78, v[242:245], s[6:7]
	s_waitcnt vmcnt(12)
	v_mul_f32_e32 v144, v26, v144
	v_mul_f32_e32 v145, v26, v145
	v_mul_f32_e32 v146, v26, v146
	v_mul_f32_e32 v147, v26, v147
	ds_write_b128 v209, v[144:147]
	v_mul_f32_e32 v148, v27, v148
	v_mul_f32_e32 v149, v27, v149
	v_mul_f32_e32 v150, v27, v150
	v_mul_f32_e32 v151, v27, v151
	ds_write_b128 v209, v[148:151] offset:1024
	v_mul_f32_e32 v152, v28, v152
	v_mul_f32_e32 v153, v28, v153
	v_mul_f32_e32 v154, v28, v154
	v_mul_f32_e32 v155, v28, v155
	ds_write_b128 v209, v[152:155] offset:2048
	v_mul_f32_e32 v156, v29, v156
	v_mul_f32_e32 v157, v29, v157
	v_mul_f32_e32 v158, v29, v158
	v_mul_f32_e32 v159, v29, v159
	ds_write_b128 v209, v[156:159] offset:3072
	v_mul_f32_e32 v160, v30, v160
	v_mul_f32_e32 v161, v30, v161
	v_mul_f32_e32 v162, v30, v162
	v_mul_f32_e32 v163, v30, v163
	ds_write_b128 v209, v[160:163] offset:4096
	v_mul_f32_e32 v164, v31, v164
	v_mul_f32_e32 v165, v31, v165
	v_mul_f32_e32 v166, v31, v166
	v_mul_f32_e32 v167, v31, v167
	ds_write_b128 v209, v[164:167] offset:5120
	v_mul_f32_e32 v168, v32, v168
	v_mul_f32_e32 v169, v32, v169
	v_mul_f32_e32 v170, v32, v170
	v_mul_f32_e32 v171, v32, v171
	ds_write_b128 v209, v[168:171] offset:6144
	v_mul_f32_e32 v172, v33, v172
	v_mul_f32_e32 v173, v33, v173
	v_mul_f32_e32 v174, v33, v174
	v_mul_f32_e32 v175, v33, v175
	ds_write_b128 v209, v[172:175] offset:7168
	s_waitcnt lgkmcnt(0)
	s_barrier
; #define GAS __attribute__((address_space(1)))
; #define LAS __attribute__((address_space(3)))
; #define LDS_WAIT() asm volatile("s_waitcnt lgkmcnt(0)" ::: "memory")
; __device__ __forceinline__ unsigned pk4_fp8(float a, float b, float c, float d) {
;     a = fminf(fmaxf(a, -448.f), 448.f); b = fminf(fmaxf(b, -448.f), 448.f); c = fminf(fmaxf(c, -448.f), 448.f); d = fminf(fmaxf(d, -448.f), 448.f);
;     int w = __builtin_amdgcn_cvt_pk_fp8_f32(a, b, 0, false); w = __builtin_amdgcn_cvt_pk_fp8_f32(c, d, w, true); return (unsigned)w; }
;     const int pr = item >> 1, kb = 2 * (pr / nblk) + (item & 1), nb = pr % nblk, k0 = 64 * kb, n0 = 32 * nb;
;     const int nr = n0 + (lane & 31); const int sc = MAP == 1 ? src_col_in(nr) : nr;
;     float v[32];
; #pragma unroll
;     for (int i = 0; i < 32; ++i) v[i] = sc >= 0 ? W[(size_t)(k0 + 2 * i + (lane >> 5)) * Nsrc + sc] : 0.f;
; #pragma unroll
;     for (int i = 0; i < 32; ++i) { const int k = k0 + 2 * i + (lane >> 5); float x = v[i] * wscale; if (KS) x *= (k < ksplit ? ksA[k] : ksB[k - ksplit]); scr[(2 * i + (lane >> 5)) * 33 + (lane & 31)] = x; }
;     LDS_WAIT(); asm volatile("" ::: "memory");
;     const int c = lane & 7;
; #pragma unroll
;     for (int j = 0; j < 4; ++j) { const int n = (lane >> 3) + 8 * j; const LAS float* s = scr + (8 * c) * 33 + n;
;         const unsigned long long o = (unsigned long long)pg8::pk4_fp8(s[0 * 33], s[1 * 33], s[2 * 33], s[3 * 33]) | ((unsigned long long)pg8::pk4_fp8(s[4 * 33], s[5 * 33], s[6 * 33], s[7 * 33]) << 32);
;         *(GAS unsigned long long*)(WT + (size_t)(n0 + n) * K + k0 + 8 * c) = o; }
;     LDS_WAIT(); asm volatile("" ::: "memory");
	s_add_u32 s8, s30, 0x6000
	s_addc_u32 s9, s31, 0
	global_load_dwordx4 v[144:147], v74, s[8:9]
	s_add_u32 s8, s8, 0x20000
	s_addc_u32 s9, s9, 0
	global_load_dwordx4 v[148:151], v74, s[8:9]
	s_add_u32 s8, s8, 0x20000
	s_addc_u32 s9, s9, 0
	global_load_dwordx4 v[152:155], v74, s[8:9]
	s_add_u32 s8, s8, 0x20000
	s_addc_u32 s9, s9, 0
	global_load_dwordx4 v[156:159], v74, s[8:9]
	s_add_u32 s8, s8, 0x20000
	s_addc_u32 s9, s9, 0
	global_load_dwordx4 v[160:163], v74, s[8:9]
	s_add_u32 s8, s8, 0x20000
	s_addc_u32 s9, s9, 0
	global_load_dwordx4 v[164:167], v74, s[8:9]
	s_add_u32 s8, s8, 0x20000
	s_addc_u32 s9, s9, 0
	global_load_dwordx4 v[168:171], v74, s[8:9]
	s_add_u32 s8, s8, 0x20000
	s_addc_u32 s9, s9, 0
	global_load_dwordx4 v[172:175], v74, s[8:9]
	s_add_u32 s6, s32, 0x1000000
	s_addc_u32 s7, s33, 0
	ds_read_b32 v226, v211
	ds_read_b32 v227, v211 offset:512
	ds_read_b32 v228, v211 offset:1024
	ds_read_b32 v229, v211 offset:1536
	ds_read_b32 v230, v211 offset:2048
	ds_read_b32 v231, v211 offset:2560
	ds_read_b32 v232, v211 offset:3072
	ds_read_b32 v233, v211 offset:3584
	ds_read_b32 v234, v211 offset:4096
	ds_read_b32 v235, v211 offset:4608
	ds_read_b32 v236, v211 offset:5120
	ds_read_b32 v237, v211 offset:5632
	ds_read_b32 v238, v211 offset:6144
	ds_read_b32 v239, v211 offset:6656
	ds_read_b32 v240, v211 offset:7168
	ds_read_b32 v241, v211 offset:7680
	s_waitcnt lgkmcnt(0)
	v_max_f32_e32 v226, v226, v226
	v_max_f32_e32 v227, v227, v227
	v_max_f32_e32 v228, v228, v228
	v_max_f32_e32 v229, v229, v229
	v_max_f32_e32 v230, v230, v230
	v_max_f32_e32 v231, v231, v231
	v_max_f32_e32 v232, v232, v232
	v_max_f32_e32 v233, v233, v233
	v_max_f32_e32 v234, v234, v234
	v_max_f32_e32 v235, v235, v235
	v_max_f32_e32 v236, v236, v236
	v_max_f32_e32 v237, v237, v237
	v_max_f32_e32 v238, v238, v238
	v_max_f32_e32 v239, v239, v239
	v_max_f32_e32 v240, v240, v240
	v_max_f32_e32 v241, v241, v241
	v_med3_f32 v226, v226, s62, v95
	v_med3_f32 v227, v227, s62, v95
	v_med3_f32 v228, v228, s62, v95
	v_med3_f32 v229, v229, s62, v95
	v_med3_f32 v230, v230, s62, v95
	v_med3_f32 v231, v231, s62, v95
	v_med3_f32 v232, v232, s62, v95
	v_med3_f32 v233, v233, s62, v95
	v_med3_f32 v234, v234, s62, v95
	v_med3_f32 v235, v235, s62, v95
	v_med3_f32 v236, v236, s62, v95
	v_med3_f32 v237, v237, s62, v95
	v_med3_f32 v238, v238, s62, v95
	v_med3_f32 v239, v239, s62, v95
	v_med3_f32 v240, v240, s62, v95
	v_med3_f32 v241, v241, s62, v95
	v_mov_b32_e32 v242, 0
	v_mov_b32_e32 v243, 0
	v_mov_b32_e32 v244, 0
	v_mov_b32_e32 v245, 0
	v_cvt_pk_fp8_f32 v242, v226, v227
	v_cvt_pk_fp8_f32 v243, v230, v231
	v_cvt_pk_fp8_f32 v244, v234, v235
	v_cvt_pk_fp8_f32 v245, v238, v239
	v_cvt_pk_fp8_f32 v242, v228, v229 op_sel:[0,0,1]
	v_cvt_pk_fp8_f32 v243, v232, v233 op_sel:[0,0,1]
	v_cvt_pk_fp8_f32 v244, v236, v237 op_sel:[0,0,1]
	v_cvt_pk_fp8_f32 v245, v240, v241 op_sel:[0,0,1]
	s_nop 0
	global_store_dwordx4 v77, v[242:245], s[6:7]
	ds_read_b32 v226, v213
	ds_read_b32 v227, v213 offset:512
	ds_read_b32 v228, v213 offset:1024
	ds_read_b32 v229, v213 offset:1536
	ds_read_b32 v230, v213 offset:2048
	ds_read_b32 v231, v213 offset:2560
	ds_read_b32 v232, v213 offset:3072
	ds_read_b32 v233, v213 offset:3584
	ds_read_b32 v234, v213 offset:4096
	ds_read_b32 v235, v213 offset:4608
	ds_read_b32 v236, v213 offset:5120
	ds_read_b32 v237, v213 offset:5632
	ds_read_b32 v238, v213 offset:6144
	ds_read_b32 v239, v213 offset:6656
	ds_read_b32 v240, v213 offset:7168
	ds_read_b32 v241, v213 offset:7680
	s_waitcnt lgkmcnt(0)
	v_max_f32_e32 v226, v226, v226
	v_max_f32_e32 v227, v227, v227
	v_max_f32_e32 v228, v228, v228
	v_max_f32_e32 v229, v229, v229
	v_max_f32_e32 v230, v230, v230
	v_max_f32_e32 v231, v231, v231
	v_max_f32_e32 v232, v232, v232
	v_max_f32_e32 v233, v233, v233
	v_max_f32_e32 v234, v234, v234
	v_max_f32_e32 v235, v235, v235
	v_max_f32_e32 v236, v236, v236
	v_max_f32_e32 v237, v237, v237
	v_max_f32_e32 v238, v238, v238
	v_max_f32_e32 v239, v239, v239
	v_max_f32_e32 v240, v240, v240
	v_max_f32_e32 v241, v241, v241
	v_med3_f32 v226, v226, s62, v95
	v_med3_f32 v227, v227, s62, v95
	v_med3_f32 v228, v228, s62, v95
	v_med3_f32 v229, v229, s62, v95
	v_med3_f32 v230, v230, s62, v95
	v_med3_f32 v231, v231, s62, v95
	v_med3_f32 v232, v232, s62, v95
	v_med3_f32 v233, v233, s62, v95
	v_med3_f32 v234, v234, s62, v95
	v_med3_f32 v235, v235, s62, v95
	v_med3_f32 v236, v236, s62, v95
	v_med3_f32 v237, v237, s62, v95
	v_med3_f32 v238, v238, s62, v95
	v_med3_f32 v239, v239, s62, v95
	v_med3_f32 v240, v240, s62, v95
	v_med3_f32 v241, v241, s62, v95
	v_mov_b32_e32 v242, 0
	v_mov_b32_e32 v243, 0
	v_mov_b32_e32 v244, 0
	v_mov_b32_e32 v245, 0
	v_cvt_pk_fp8_f32 v242, v226, v227
	v_cvt_pk_fp8_f32 v243, v230, v231
	v_cvt_pk_fp8_f32 v244, v234, v235
	v_cvt_pk_fp8_f32 v245, v238, v239
	v_cvt_pk_fp8_f32 v242, v228, v229 op_sel:[0,0,1]
	v_cvt_pk_fp8_f32 v243, v232, v233 op_sel:[0,0,1]
	v_cvt_pk_fp8_f32 v244, v236, v237 op_sel:[0,0,1]
	v_cvt_pk_fp8_f32 v245, v240, v241 op_sel:[0,0,1]
	s_nop 0
	global_store_dwordx4 v78, v[242:245], s[6:7]
	s_waitcnt vmcnt(12)
	v_mul_f32_e32 v176, v26, v176
	v_mul_f32_e32 v177, v26, v177
	v_mul_f32_e32 v178, v26, v178
	v_mul_f32_e32 v179, v26, v179
	ds_write_b128 v210, v[176:179]
	v_mul_f32_e32 v180, v27, v180
	v_mul_f32_e32 v181, v27, v181
	v_mul_f32_e32 v182, v27, v182
	v_mul_f32_e32 v183, v27, v183
	ds_write_b128 v210, v[180:183] offset:1024
	v_mul_f32_e32 v184, v28, v184
	v_mul_f32_e32 v185, v28, v185
	v_mul_f32_e32 v186, v28, v186
	v_mul_f32_e32 v187, v28, v187
	ds_write_b128 v210, v[184:187] offset:2048
	v_mul_f32_e32 v188, v29, v188
	v_mul_f32_e32 v189, v29, v189
	v_mul_f32_e32 v190, v29, v190
	v_mul_f32_e32 v191, v29, v191
	ds_write_b128 v210, v[188:191] offset:3072
	v_mul_f32_e32 v192, v30, v192
	v_mul_f32_e32 v193, v30, v193
	v_mul_f32_e32 v194, v30, v194
	v_mul_f32_e32 v195, v30, v195
	ds_write_b128 v210, v[192:195] offset:4096
	v_mul_f32_e32 v196, v31, v196
	v_mul_f32_e32 v197, v31, v197
	v_mul_f32_e32 v198, v31, v198
	v_mul_f32_e32 v199, v31, v199
	ds_write_b128 v210, v[196:199] offset:5120
	v_mul_f32_e32 v200, v32, v200
	v_mul_f32_e32 v201, v32, v201
	v_mul_f32_e32 v202, v32, v202
	v_mul_f32_e32 v203, v32, v203
	ds_write_b128 v210, v[200:203] offset:6144
	v_mul_f32_e32 v204, v33, v204
	v_mul_f32_e32 v205, v33, v205
	v_mul_f32_e32 v206, v33, v206
	v_mul_f32_e32 v207, v33, v207
	ds_write_b128 v210, v[204:207] offset:7168
	s_waitcnt lgkmcnt(0)
	s_barrier
; #define GAS __attribute__((address_space(1)))
; #define LAS __attribute__((address_space(3)))
; #define LDS_WAIT() asm volatile("s_waitcnt lgkmcnt(0)" ::: "memory")
; __device__ __forceinline__ unsigned pk4_fp8(float a, float b, float c, float d) {
;     a = fminf(fmaxf(a, -448.f), 448.f); b = fminf(fmaxf(b, -448.f), 448.f); c = fminf(fmaxf(c, -448.f), 448.f); d = fminf(fmaxf(d, -448.f), 448.f);
;     int w = __builtin_amdgcn_cvt_pk_fp8_f32(a, b, 0, false); w = __builtin_amdgcn_cvt_pk_fp8_f32(c, d, w, true); return (unsigned)w; }
;     const int pr = item >> 1, kb = 2 * (pr / nblk) + (item & 1), nb = pr % nblk, k0 = 64 * kb, n0 = 32 * nb;
;     const int nr = n0 + (lane & 31); const int sc = MAP == 1 ? src_col_in(nr) : nr;
;     float v[32];
; #pragma unroll
;     for (int i = 0; i < 32; ++i) v[i] = sc >= 0 ? W[(size_t)(k0 + 2 * i + (lane >> 5)) * Nsrc + sc] : 0.f;
; #pragma unroll
;     for (int i = 0; i < 32; ++i) { const int k = k0 + 2 * i + (lane >> 5); float x = v[i] * wscale; if (KS) x *= (k < ksplit ? ksA[k] : ksB[k - ksplit]); scr[(2 * i + (lane >> 5)) * 33 + (lane & 31)] = x; }
;     LDS_WAIT(); asm volatile("" ::: "memory");
;     const int c = lane & 7;
; #pragma unroll
;     for (int j = 0; j < 4; ++j) { const int n = (lane >> 3) + 8 * j; const LAS float* s = scr + (8 * c) * 33 + n;
;         const unsigned long long o = (unsigned long long)pg8::pk4_fp8(s[0 * 33], s[1 * 33], s[2 * 33], s[3 * 33]) | ((unsigned long long)pg8::pk4_fp8(s[4 * 33], s[5 * 33], s[6 * 33], s[7 * 33]) << 32);
;         *(GAS unsigned long long*)(WT + (size_t)(n0 + n) * K + k0 + 8 * c) = o; }
;     LDS_WAIT(); asm volatile("" ::: "memory");
	s_add_u32 s8, s30, 0x7000
	s_addc_u32 s9, s31, 0
	global_load_dwordx4 v[176:179], v74, s[8:9]
	s_add_u32 s8, s8, 0x20000
	s_addc_u32 s9, s9, 0
	global_load_dwordx4 v[180:183], v74, s[8:9]
	s_add_u32 s8, s8, 0x20000
	s_addc_u32 s9, s9, 0
	global_load_dwordx4 v[184:187], v74, s[8:9]
	s_add_u32 s8, s8, 0x20000
	s_addc_u32 s9, s9, 0
	global_load_dwordx4 v[188:191], v74, s[8:9]
	s_add_u32 s8, s8, 0x20000
	s_addc_u32 s9, s9, 0
	global_load_dwordx4 v[192:195], v74, s[8:9]
	s_add_u32 s8, s8, 0x20000
	s_addc_u32 s9, s9, 0
	global_load_dwordx4 v[196:199], v74, s[8:9]
	s_add_u32 s8, s8, 0x20000
	s_addc_u32 s9, s9, 0
	global_load_dwordx4 v[200:203], v74, s[8:9]
	s_add_u32 s8, s8, 0x20000
	s_addc_u32 s9, s9, 0
	global_load_dwordx4 v[204:207], v74, s[8:9]
	s_add_u32 s6, s32, 0x1400000
	s_addc_u32 s7, s33, 0
	ds_read_b32 v226, v212
	ds_read_b32 v227, v212 offset:512
	ds_read_b32 v228, v212 offset:1024
	ds_read_b32 v229, v212 offset:1536
	ds_read_b32 v230, v212 offset:2048
	ds_read_b32 v231, v212 offset:2560
	ds_read_b32 v232, v212 offset:3072
	ds_read_b32 v233, v212 offset:3584
	ds_read_b32 v234, v212 offset:4096
	ds_read_b32 v235, v212 offset:4608
	ds_read_b32 v236, v212 offset:5120
	ds_read_b32 v237, v212 offset:5632
	ds_read_b32 v238, v212 offset:6144
	ds_read_b32 v239, v212 offset:6656
	ds_read_b32 v240, v212 offset:7168
	ds_read_b32 v241, v212 offset:7680
	s_waitcnt lgkmcnt(0)
	v_max_f32_e32 v226, v226, v226
	v_max_f32_e32 v227, v227, v227
	v_max_f32_e32 v228, v228, v228
	v_max_f32_e32 v229, v229, v229
	v_max_f32_e32 v230, v230, v230
	v_max_f32_e32 v231, v231, v231
	v_max_f32_e32 v232, v232, v232
	v_max_f32_e32 v233, v233, v233
	v_max_f32_e32 v234, v234, v234
	v_max_f32_e32 v235, v235, v235
	v_max_f32_e32 v236, v236, v236
	v_max_f32_e32 v237, v237, v237
	v_max_f32_e32 v238, v238, v238
	v_max_f32_e32 v239, v239, v239
	v_max_f32_e32 v240, v240, v240
	v_max_f32_e32 v241, v241, v241
	v_med3_f32 v226, v226, s62, v95
	v_med3_f32 v227, v227, s62, v95
	v_med3_f32 v228, v228, s62, v95
	v_med3_f32 v229, v229, s62, v95
	v_med3_f32 v230, v230, s62, v95
	v_med3_f32 v231, v231, s62, v95
	v_med3_f32 v232, v232, s62, v95
	v_med3_f32 v233, v233, s62, v95
	v_med3_f32 v234, v234, s62, v95
	v_med3_f32 v235, v235, s62, v95
	v_med3_f32 v236, v236, s62, v95
	v_med3_f32 v237, v237, s62, v95
	v_med3_f32 v238, v238, s62, v95
	v_med3_f32 v239, v239, s62, v95
	v_med3_f32 v240, v240, s62, v95
	v_med3_f32 v241, v241, s62, v95
	v_mov_b32_e32 v242, 0
	v_mov_b32_e32 v243, 0
	v_mov_b32_e32 v244, 0
	v_mov_b32_e32 v245, 0
	v_cvt_pk_fp8_f32 v242, v226, v227
	v_cvt_pk_fp8_f32 v243, v230, v231
	v_cvt_pk_fp8_f32 v244, v234, v235
	v_cvt_pk_fp8_f32 v245, v238, v239
	v_cvt_pk_fp8_f32 v242, v228, v229 op_sel:[0,0,1]
	v_cvt_pk_fp8_f32 v243, v232, v233 op_sel:[0,0,1]
	v_cvt_pk_fp8_f32 v244, v236, v237 op_sel:[0,0,1]
	v_cvt_pk_fp8_f32 v245, v240, v241 op_sel:[0,0,1]
	s_nop 0
	global_store_dwordx4 v77, v[242:245], s[6:7]
	ds_read_b32 v226, v214
	ds_read_b32 v227, v214 offset:512
	ds_read_b32 v228, v214 offset:1024
	ds_read_b32 v229, v214 offset:1536
	ds_read_b32 v230, v214 offset:2048
	ds_read_b32 v231, v214 offset:2560
	ds_read_b32 v232, v214 offset:3072
	ds_read_b32 v233, v214 offset:3584
	ds_read_b32 v234, v214 offset:4096
	ds_read_b32 v235, v214 offset:4608
	ds_read_b32 v236, v214 offset:5120
	ds_read_b32 v237, v214 offset:5632
	ds_read_b32 v238, v214 offset:6144
	ds_read_b32 v239, v214 offset:6656
	ds_read_b32 v240, v214 offset:7168
	ds_read_b32 v241, v214 offset:7680
	s_waitcnt lgkmcnt(0)
	v_max_f32_e32 v226, v226, v226
	v_max_f32_e32 v227, v227, v227
	v_max_f32_e32 v228, v228, v228
	v_max_f32_e32 v229, v229, v229
	v_max_f32_e32 v230, v230, v230
	v_max_f32_e32 v231, v231, v231
	v_max_f32_e32 v232, v232, v232
	v_max_f32_e32 v233, v233, v233
	v_max_f32_e32 v234, v234, v234
	v_max_f32_e32 v235, v235, v235
	v_max_f32_e32 v236, v236, v236
	v_max_f32_e32 v237, v237, v237
	v_max_f32_e32 v238, v238, v238
	v_max_f32_e32 v239, v239, v239
	v_max_f32_e32 v240, v240, v240
	v_max_f32_e32 v241, v241, v241
	v_med3_f32 v226, v226, s62, v95
	v_med3_f32 v227, v227, s62, v95
	v_med3_f32 v228, v228, s62, v95
	v_med3_f32 v229, v229, s62, v95
	v_med3_f32 v230, v230, s62, v95
	v_med3_f32 v231, v231, s62, v95
	v_med3_f32 v232, v232, s62, v95
	v_med3_f32 v233, v233, s62, v95
	v_med3_f32 v234, v234, s62, v95
	v_med3_f32 v235, v235, s62, v95
	v_med3_f32 v236, v236, s62, v95
	v_med3_f32 v237, v237, s62, v95
	v_med3_f32 v238, v238, s62, v95
	v_med3_f32 v239, v239, s62, v95
	v_med3_f32 v240, v240, s62, v95
	v_med3_f32 v241, v241, s62, v95
	v_mov_b32_e32 v242, 0
	v_mov_b32_e32 v243, 0
	v_mov_b32_e32 v244, 0
	v_mov_b32_e32 v245, 0
	v_cvt_pk_fp8_f32 v242, v226, v227
	v_cvt_pk_fp8_f32 v243, v230, v231
	v_cvt_pk_fp8_f32 v244, v234, v235
	v_cvt_pk_fp8_f32 v245, v238, v239
	v_cvt_pk_fp8_f32 v242, v228, v229 op_sel:[0,0,1]
	v_cvt_pk_fp8_f32 v243, v232, v233 op_sel:[0,0,1]
	v_cvt_pk_fp8_f32 v244, v236, v237 op_sel:[0,0,1]
	v_cvt_pk_fp8_f32 v245, v240, v241 op_sel:[0,0,1]
	s_nop 0
	global_store_dwordx4 v78, v[242:245], s[6:7]
	s_waitcnt vmcnt(12)
	v_mul_f32_e32 v144, v26, v144
	v_mul_f32_e32 v145, v26, v145
	v_mul_f32_e32 v146, v26, v146
	v_mul_f32_e32 v147, v26, v147
	ds_write_b128 v209, v[144:147]
	v_mul_f32_e32 v148, v27, v148
	v_mul_f32_e32 v149, v27, v149
	v_mul_f32_e32 v150, v27, v150
	v_mul_f32_e32 v151, v27, v151
	ds_write_b128 v209, v[148:151] offset:1024
	v_mul_f32_e32 v152, v28, v152
	v_mul_f32_e32 v153, v28, v153
	v_mul_f32_e32 v154, v28, v154
	v_mul_f32_e32 v155, v28, v155
	ds_write_b128 v209, v[152:155] offset:2048
	v_mul_f32_e32 v156, v29, v156
	v_mul_f32_e32 v157, v29, v157
	v_mul_f32_e32 v158, v29, v158
	v_mul_f32_e32 v159, v29, v159
	ds_write_b128 v209, v[156:159] offset:3072
	v_mul_f32_e32 v160, v30, v160
	v_mul_f32_e32 v161, v30, v161
	v_mul_f32_e32 v162, v30, v162
	v_mul_f32_e32 v163, v30, v163
	ds_write_b128 v209, v[160:163] offset:4096
	v_mul_f32_e32 v164, v31, v164
	v_mul_f32_e32 v165, v31, v165
	v_mul_f32_e32 v166, v31, v166
	v_mul_f32_e32 v167, v31, v167
	ds_write_b128 v209, v[164:167] offset:5120
	v_mul_f32_e32 v168, v32, v168
	v_mul_f32_e32 v169, v32, v169
	v_mul_f32_e32 v170, v32, v170
	v_mul_f32_e32 v171, v32, v171
	ds_write_b128 v209, v[168:171] offset:6144
	v_mul_f32_e32 v172, v33, v172
	v_mul_f32_e32 v173, v33, v173
	v_mul_f32_e32 v174, v33, v174
	v_mul_f32_e32 v175, v33, v175
	ds_write_b128 v209, v[172:175] offset:7168
	s_waitcnt lgkmcnt(0)
	s_barrier
; #define GAS __attribute__((address_space(1)))
; #define LAS __attribute__((address_space(3)))
; #define LDS_WAIT() asm volatile("s_waitcnt lgkmcnt(0)" ::: "memory")
; __device__ __forceinline__ unsigned pk4_fp8(float a, float b, float c, float d) {
;     a = fminf(fmaxf(a, -448.f), 448.f); b = fminf(fmaxf(b, -448.f), 448.f); c = fminf(fmaxf(c, -448.f), 448.f); d = fminf(fmaxf(d, -448.f), 448.f);
;     int w = __builtin_amdgcn_cvt_pk_fp8_f32(a, b, 0, false); w = __builtin_amdgcn_cvt_pk_fp8_f32(c, d, w, true); return (unsigned)w; }
;     const int pr = item >> 1, kb = 2 * (pr / nblk) + (item & 1), nb = pr % nblk, k0 = 64 * kb, n0 = 32 * nb;
;     const int nr = n0 + (lane & 31); const int sc = MAP == 1 ? src_col_in(nr) : nr;
;     float v[32];
; #pragma unroll
;     for (int i = 0; i < 32; ++i) v[i] = sc >= 0 ? W[(size_t)(k0 + 2 * i + (lane >> 5)) * Nsrc + sc] : 0.f;
; #pragma unroll
;     for (int i = 0; i < 32; ++i) { const int k = k0 + 2 * i + (lane >> 5); float x = v[i] * wscale; if (KS) x *= (k < ksplit ? ksA[k] : ksB[k - ksplit]); scr[(2 * i + (lane >> 5)) * 33 + (lane & 31)] = x; }
;     LDS_WAIT(); asm volatile("" ::: "memory");
;     const int c = lane & 7;
; #pragma unroll
;     for (int j = 0; j < 4; ++j) { const int n = (lane >> 3) + 8 * j; const LAS float* s = scr + (8 * c) * 33 + n;
;         const unsigned long long o = (unsigned long long)pg8::pk4_fp8(s[0 * 33], s[1 * 33], s[2 * 33], s[3 * 33]) | ((unsigned long long)pg8::pk4_fp8(s[4 * 33], s[5 * 33], s[6 * 33], s[7 * 33]) << 32);
;         *(GAS unsigned long long*)(WT + (size_t)(n0 + n) * K + k0 + 8 * c) = o; }
;     LDS_WAIT(); asm volatile("" ::: "memory");
	s_add_u32 s8, s30, 0x8000
	s_addc_u32 s9, s31, 0
	global_load_dwordx4 v[144:147], v74, s[8:9]
	s_add_u32 s8, s8, 0x20000
	s_addc_u32 s9, s9, 0
	global_load_dwordx4 v[148:151], v74, s[8:9]
	s_add_u32 s8, s8, 0x20000
	s_addc_u32 s9, s9, 0
	global_load_dwordx4 v[152:155], v74, s[8:9]
	s_add_u32 s8, s8, 0x20000
	s_addc_u32 s9, s9, 0
	global_load_dwordx4 v[156:159], v74, s[8:9]
	s_add_u32 s8, s8, 0x20000
	s_addc_u32 s9, s9, 0
	global_load_dwordx4 v[160:163], v74, s[8:9]
	s_add_u32 s8, s8, 0x20000
	s_addc_u32 s9, s9, 0
	global_load_dwordx4 v[164:167], v74, s[8:9]
	s_add_u32 s8, s8, 0x20000
	s_addc_u32 s9, s9, 0
	global_load_dwordx4 v[168:171], v74, s[8:9]
	s_add_u32 s8, s8, 0x20000
	s_addc_u32 s9, s9, 0
	global_load_dwordx4 v[172:175], v74, s[8:9]
	s_add_u32 s6, s32, 0x1800000
	s_addc_u32 s7, s33, 0
	ds_read_b32 v226, v211
	ds_read_b32 v227, v211 offset:512
	ds_read_b32 v228, v211 offset:1024
	ds_read_b32 v229, v211 offset:1536
	ds_read_b32 v230, v211 offset:2048
	ds_read_b32 v231, v211 offset:2560
	ds_read_b32 v232, v211 offset:3072
	ds_read_b32 v233, v211 offset:3584
	ds_read_b32 v234, v211 offset:4096
	ds_read_b32 v235, v211 offset:4608
	ds_read_b32 v236, v211 offset:5120
	ds_read_b32 v237, v211 offset:5632
	ds_read_b32 v238, v211 offset:6144
	ds_read_b32 v239, v211 offset:6656
	ds_read_b32 v240, v211 offset:7168
	ds_read_b32 v241, v211 offset:7680
	s_waitcnt lgkmcnt(0)
	v_max_f32_e32 v226, v226, v226
	v_max_f32_e32 v227, v227, v227
	v_max_f32_e32 v228, v228, v228
	v_max_f32_e32 v229, v229, v229
	v_max_f32_e32 v230, v230, v230
	v_max_f32_e32 v231, v231, v231
	v_max_f32_e32 v232, v232, v232
	v_max_f32_e32 v233, v233, v233
	v_max_f32_e32 v234, v234, v234
	v_max_f32_e32 v235, v235, v235
	v_max_f32_e32 v236, v236, v236
	v_max_f32_e32 v237, v237, v237
	v_max_f32_e32 v238, v238, v238
	v_max_f32_e32 v239, v239, v239
	v_max_f32_e32 v240, v240, v240
	v_max_f32_e32 v241, v241, v241
	v_med3_f32 v226, v226, s62, v95
	v_med3_f32 v227, v227, s62, v95
	v_med3_f32 v228, v228, s62, v95
	v_med3_f32 v229, v229, s62, v95
	v_med3_f32 v230, v230, s62, v95
	v_med3_f32 v231, v231, s62, v95
	v_med3_f32 v232, v232, s62, v95
	v_med3_f32 v233, v233, s62, v95
	v_med3_f32 v234, v234, s62, v95
	v_med3_f32 v235, v235, s62, v95
	v_med3_f32 v236, v236, s62, v95
	v_med3_f32 v237, v237, s62, v95
	v_med3_f32 v238, v238, s62, v95
	v_med3_f32 v239, v239, s62, v95
	v_med3_f32 v240, v240, s62, v95
	v_med3_f32 v241, v241, s62, v95
	v_mov_b32_e32 v242, 0
	v_mov_b32_e32 v243, 0
	v_mov_b32_e32 v244, 0
	v_mov_b32_e32 v245, 0
	v_cvt_pk_fp8_f32 v242, v226, v227
	v_cvt_pk_fp8_f32 v243, v230, v231
	v_cvt_pk_fp8_f32 v244, v234, v235
	v_cvt_pk_fp8_f32 v245, v238, v239
	v_cvt_pk_fp8_f32 v242, v228, v229 op_sel:[0,0,1]
	v_cvt_pk_fp8_f32 v243, v232, v233 op_sel:[0,0,1]
	v_cvt_pk_fp8_f32 v244, v236, v237 op_sel:[0,0,1]
	v_cvt_pk_fp8_f32 v245, v240, v241 op_sel:[0,0,1]
	s_nop 0
	global_store_dwordx4 v77, v[242:245], s[6:7]
	ds_read_b32 v226, v213
	ds_read_b32 v227, v213 offset:512
	ds_read_b32 v228, v213 offset:1024
	ds_read_b32 v229, v213 offset:1536
	ds_read_b32 v230, v213 offset:2048
	ds_read_b32 v231, v213 offset:2560
	ds_read_b32 v232, v213 offset:3072
	ds_read_b32 v233, v213 offset:3584
	ds_read_b32 v234, v213 offset:4096
	ds_read_b32 v235, v213 offset:4608
	ds_read_b32 v236, v213 offset:5120
	ds_read_b32 v237, v213 offset:5632
	ds_read_b32 v238, v213 offset:6144
	ds_read_b32 v239, v213 offset:6656
	ds_read_b32 v240, v213 offset:7168
	ds_read_b32 v241, v213 offset:7680
	s_waitcnt lgkmcnt(0)
	v_max_f32_e32 v226, v226, v226
	v_max_f32_e32 v227, v227, v227
	v_max_f32_e32 v228, v228, v228
	v_max_f32_e32 v229, v229, v229
	v_max_f32_e32 v230, v230, v230
	v_max_f32_e32 v231, v231, v231
	v_max_f32_e32 v232, v232, v232
	v_max_f32_e32 v233, v233, v233
	v_max_f32_e32 v234, v234, v234
	v_max_f32_e32 v235, v235, v235
	v_max_f32_e32 v236, v236, v236
	v_max_f32_e32 v237, v237, v237
	v_max_f32_e32 v238, v238, v238
	v_max_f32_e32 v239, v239, v239
	v_max_f32_e32 v240, v240, v240
	v_max_f32_e32 v241, v241, v241
	v_med3_f32 v226, v226, s62, v95
	v_med3_f32 v227, v227, s62, v95
	v_med3_f32 v228, v228, s62, v95
	v_med3_f32 v229, v229, s62, v95
	v_med3_f32 v230, v230, s62, v95
	v_med3_f32 v231, v231, s62, v95
	v_med3_f32 v232, v232, s62, v95
	v_med3_f32 v233, v233, s62, v95
	v_med3_f32 v234, v234, s62, v95
	v_med3_f32 v235, v235, s62, v95
	v_med3_f32 v236, v236, s62, v95
	v_med3_f32 v237, v237, s62, v95
	v_med3_f32 v238, v238, s62, v95
	v_med3_f32 v239, v239, s62, v95
	v_med3_f32 v240, v240, s62, v95
	v_med3_f32 v241, v241, s62, v95
	v_mov_b32_e32 v242, 0
	v_mov_b32_e32 v243, 0
	v_mov_b32_e32 v244, 0
	v_mov_b32_e32 v245, 0
	v_cvt_pk_fp8_f32 v242, v226, v227
	v_cvt_pk_fp8_f32 v243, v230, v231
	v_cvt_pk_fp8_f32 v244, v234, v235
	v_cvt_pk_fp8_f32 v245, v238, v239
	v_cvt_pk_fp8_f32 v242, v228, v229 op_sel:[0,0,1]
	v_cvt_pk_fp8_f32 v243, v232, v233 op_sel:[0,0,1]
	v_cvt_pk_fp8_f32 v244, v236, v237 op_sel:[0,0,1]
	v_cvt_pk_fp8_f32 v245, v240, v241 op_sel:[0,0,1]
	s_nop 0
	global_store_dwordx4 v78, v[242:245], s[6:7]
	s_waitcnt vmcnt(12)
	v_mul_f32_e32 v176, v26, v176
	v_mul_f32_e32 v177, v26, v177
	v_mul_f32_e32 v178, v26, v178
	v_mul_f32_e32 v179, v26, v179
	ds_write_b128 v210, v[176:179]
	v_mul_f32_e32 v180, v27, v180
	v_mul_f32_e32 v181, v27, v181
	v_mul_f32_e32 v182, v27, v182
	v_mul_f32_e32 v183, v27, v183
	ds_write_b128 v210, v[180:183] offset:1024
	v_mul_f32_e32 v184, v28, v184
	v_mul_f32_e32 v185, v28, v185
	v_mul_f32_e32 v186, v28, v186
	v_mul_f32_e32 v187, v28, v187
	ds_write_b128 v210, v[184:187] offset:2048
	v_mul_f32_e32 v188, v29, v188
	v_mul_f32_e32 v189, v29, v189
	v_mul_f32_e32 v190, v29, v190
	v_mul_f32_e32 v191, v29, v191
	ds_write_b128 v210, v[188:191] offset:3072
	v_mul_f32_e32 v192, v30, v192
	v_mul_f32_e32 v193, v30, v193
	v_mul_f32_e32 v194, v30, v194
	v_mul_f32_e32 v195, v30, v195
	ds_write_b128 v210, v[192:195] offset:4096
	v_mul_f32_e32 v196, v31, v196
	v_mul_f32_e32 v197, v31, v197
	v_mul_f32_e32 v198, v31, v198
	v_mul_f32_e32 v199, v31, v199
	ds_write_b128 v210, v[196:199] offset:5120
	v_mul_f32_e32 v200, v32, v200
	v_mul_f32_e32 v201, v32, v201
	v_mul_f32_e32 v202, v32, v202
	v_mul_f32_e32 v203, v32, v203
	ds_write_b128 v210, v[200:203] offset:6144
	v_mul_f32_e32 v204, v33, v204
	v_mul_f32_e32 v205, v33, v205
	v_mul_f32_e32 v206, v33, v206
	v_mul_f32_e32 v207, v33, v207
	ds_write_b128 v210, v[204:207] offset:7168
	s_waitcnt lgkmcnt(0)
	s_barrier
; #define GAS __attribute__((address_space(1)))
; #define LAS __attribute__((address_space(3)))
; #define LDS_WAIT() asm volatile("s_waitcnt lgkmcnt(0)" ::: "memory")
; __device__ __forceinline__ unsigned pk4_fp8(float a, float b, float c, float d) {
;     a = fminf(fmaxf(a, -448.f), 448.f); b = fminf(fmaxf(b, -448.f), 448.f); c = fminf(fmaxf(c, -448.f), 448.f); d = fminf(fmaxf(d, -448.f), 448.f);
;     int w = __builtin_amdgcn_cvt_pk_fp8_f32(a, b, 0, false); w = __builtin_amdgcn_cvt_pk_fp8_f32(c, d, w, true); return (unsigned)w; }
;     const int pr = item >> 1, kb = 2 * (pr / nblk) + (item & 1), nb = pr % nblk, k0 = 64 * kb, n0 = 32 * nb;
;     const int nr = n0 + (lane & 31); const int sc = MAP == 1 ? src_col_in(nr) : nr;
;     float v[32];
; #pragma unroll
;     for (int i = 0; i < 32; ++i) v[i] = sc >= 0 ? W[(size_t)(k0 + 2 * i + (lane >> 5)) * Nsrc + sc] : 0.f;
; #pragma unroll
;     for (int i = 0; i < 32; ++i) { const int k = k0 + 2 * i + (lane >> 5); float x = v[i] * wscale; if (KS) x *= (k < ksplit ? ksA[k] : ksB[k - ksplit]); scr[(2 * i + (lane >> 5)) * 33 + (lane & 31)] = x; }
;     LDS_WAIT(); asm volatile("" ::: "memory");
;     const int c = lane & 7;
; #pragma unroll
;     for (int j = 0; j < 4; ++j) { const int n = (lane >> 3) + 8 * j; const LAS float* s = scr + (8 * c) * 33 + n;
;         const unsigned long long o = (unsigned long long)pg8::pk4_fp8(s[0 * 33], s[1 * 33], s[2 * 33], s[3 * 33]) | ((unsigned long long)pg8::pk4_fp8(s[4 * 33], s[5 * 33], s[6 * 33], s[7 * 33]) << 32);
;         *(GAS unsigned long long*)(WT + (size_t)(n0 + n) * K + k0 + 8 * c) = o; }
;     LDS_WAIT(); asm volatile("" ::: "memory");
	s_add_u32 s8, s30, 0x9000
	s_addc_u32 s9, s31, 0
	global_load_dwordx4 v[176:179], v74, s[8:9]
	s_add_u32 s8, s8, 0x20000
	s_addc_u32 s9, s9, 0
	global_load_dwordx4 v[180:183], v74, s[8:9]
	s_add_u32 s8, s8, 0x20000
	s_addc_u32 s9, s9, 0
	global_load_dwordx4 v[184:187], v74, s[8:9]
	s_add_u32 s8, s8, 0x20000
	s_addc_u32 s9, s9, 0
	global_load_dwordx4 v[188:191], v74, s[8:9]
	s_add_u32 s8, s8, 0x20000
	s_addc_u32 s9, s9, 0
	global_load_dwordx4 v[192:195], v74, s[8:9]
	s_add_u32 s8, s8, 0x20000
	s_addc_u32 s9, s9, 0
	global_load_dwordx4 v[196:199], v74, s[8:9]
	s_add_u32 s8, s8, 0x20000
	s_addc_u32 s9, s9, 0
	global_load_dwordx4 v[200:203], v74, s[8:9]
	s_add_u32 s8, s8, 0x20000
	s_addc_u32 s9, s9, 0
	global_load_dwordx4 v[204:207], v74, s[8:9]
	s_add_u32 s6, s32, 0x1c00000
	s_addc_u32 s7, s33, 0
	ds_read_b32 v226, v212
	ds_read_b32 v227, v212 offset:512
	ds_read_b32 v228, v212 offset:1024
	ds_read_b32 v229, v212 offset:1536
	ds_read_b32 v230, v212 offset:2048
	ds_read_b32 v231, v212 offset:2560
	ds_read_b32 v232, v212 offset:3072
	ds_read_b32 v233, v212 offset:3584
	ds_read_b32 v234, v212 offset:4096
	ds_read_b32 v235, v212 offset:4608
	ds_read_b32 v236, v212 offset:5120
	ds_read_b32 v237, v212 offset:5632
	ds_read_b32 v238, v212 offset:6144
	ds_read_b32 v239, v212 offset:6656
	ds_read_b32 v240, v212 offset:7168
	ds_read_b32 v241, v212 offset:7680
	s_waitcnt lgkmcnt(0)
	v_max_f32_e32 v226, v226, v226
	v_max_f32_e32 v227, v227, v227
	v_max_f32_e32 v228, v228, v228
	v_max_f32_e32 v229, v229, v229
	v_max_f32_e32 v230, v230, v230
	v_max_f32_e32 v231, v231, v231
	v_max_f32_e32 v232, v232, v232
	v_max_f32_e32 v233, v233, v233
	v_max_f32_e32 v234, v234, v234
	v_max_f32_e32 v235, v235, v235
	v_max_f32_e32 v236, v236, v236
	v_max_f32_e32 v237, v237, v237
	v_max_f32_e32 v238, v238, v238
	v_max_f32_e32 v239, v239, v239
	v_max_f32_e32 v240, v240, v240
	v_max_f32_e32 v241, v241, v241
	v_med3_f32 v226, v226, s62, v95
	v_med3_f32 v227, v227, s62, v95
	v_med3_f32 v228, v228, s62, v95
	v_med3_f32 v229, v229, s62, v95
	v_med3_f32 v230, v230, s62, v95
	v_med3_f32 v231, v231, s62, v95
	v_med3_f32 v232, v232, s62, v95
	v_med3_f32 v233, v233, s62, v95
	v_med3_f32 v234, v234, s62, v95
	v_med3_f32 v235, v235, s62, v95
	v_med3_f32 v236, v236, s62, v95
	v_med3_f32 v237, v237, s62, v95
	v_med3_f32 v238, v238, s62, v95
	v_med3_f32 v239, v239, s62, v95
	v_med3_f32 v240, v240, s62, v95
	v_med3_f32 v241, v241, s62, v95
	v_mov_b32_e32 v242, 0
	v_mov_b32_e32 v243, 0
	v_mov_b32_e32 v244, 0
	v_mov_b32_e32 v245, 0
	v_cvt_pk_fp8_f32 v242, v226, v227
	v_cvt_pk_fp8_f32 v243, v230, v231
	v_cvt_pk_fp8_f32 v244, v234, v235
	v_cvt_pk_fp8_f32 v245, v238, v239
	v_cvt_pk_fp8_f32 v242, v228, v229 op_sel:[0,0,1]
	v_cvt_pk_fp8_f32 v243, v232, v233 op_sel:[0,0,1]
	v_cvt_pk_fp8_f32 v244, v236, v237 op_sel:[0,0,1]
	v_cvt_pk_fp8_f32 v245, v240, v241 op_sel:[0,0,1]
	s_nop 0
	global_store_dwordx4 v77, v[242:245], s[6:7]
	ds_read_b32 v226, v214
	ds_read_b32 v227, v214 offset:512
	ds_read_b32 v228, v214 offset:1024
	ds_read_b32 v229, v214 offset:1536
	ds_read_b32 v230, v214 offset:2048
	ds_read_b32 v231, v214 offset:2560
	ds_read_b32 v232, v214 offset:3072
	ds_read_b32 v233, v214 offset:3584
	ds_read_b32 v234, v214 offset:4096
	ds_read_b32 v235, v214 offset:4608
	ds_read_b32 v236, v214 offset:5120
	ds_read_b32 v237, v214 offset:5632
	ds_read_b32 v238, v214 offset:6144
	ds_read_b32 v239, v214 offset:6656
	ds_read_b32 v240, v214 offset:7168
	ds_read_b32 v241, v214 offset:7680
	s_waitcnt lgkmcnt(0)
	v_max_f32_e32 v226, v226, v226
	v_max_f32_e32 v227, v227, v227
	v_max_f32_e32 v228, v228, v228
	v_max_f32_e32 v229, v229, v229
	v_max_f32_e32 v230, v230, v230
	v_max_f32_e32 v231, v231, v231
	v_max_f32_e32 v232, v232, v232
	v_max_f32_e32 v233, v233, v233
	v_max_f32_e32 v234, v234, v234
	v_max_f32_e32 v235, v235, v235
	v_max_f32_e32 v236, v236, v236
	v_max_f32_e32 v237, v237, v237
	v_max_f32_e32 v238, v238, v238
	v_max_f32_e32 v239, v239, v239
	v_max_f32_e32 v240, v240, v240
	v_max_f32_e32 v241, v241, v241
	v_med3_f32 v226, v226, s62, v95
	v_med3_f32 v227, v227, s62, v95
	v_med3_f32 v228, v228, s62, v95
	v_med3_f32 v229, v229, s62, v95
	v_med3_f32 v230, v230, s62, v95
	v_med3_f32 v231, v231, s62, v95
	v_med3_f32 v232, v232, s62, v95
	v_med3_f32 v233, v233, s62, v95
	v_med3_f32 v234, v234, s62, v95
	v_med3_f32 v235, v235, s62, v95
	v_med3_f32 v236, v236, s62, v95
	v_med3_f32 v237, v237, s62, v95
	v_med3_f32 v238, v238, s62, v95
	v_med3_f32 v239, v239, s62, v95
	v_med3_f32 v240, v240, s62, v95
	v_med3_f32 v241, v241, s62, v95
	v_mov_b32_e32 v242, 0
	v_mov_b32_e32 v243, 0
	v_mov_b32_e32 v244, 0
	v_mov_b32_e32 v245, 0
	v_cvt_pk_fp8_f32 v242, v226, v227
	v_cvt_pk_fp8_f32 v243, v230, v231
	v_cvt_pk_fp8_f32 v244, v234, v235
	v_cvt_pk_fp8_f32 v245, v238, v239
	v_cvt_pk_fp8_f32 v242, v228, v229 op_sel:[0,0,1]
	v_cvt_pk_fp8_f32 v243, v232, v233 op_sel:[0,0,1]
	v_cvt_pk_fp8_f32 v244, v236, v237 op_sel:[0,0,1]
	v_cvt_pk_fp8_f32 v245, v240, v241 op_sel:[0,0,1]
	s_nop 0
	global_store_dwordx4 v78, v[242:245], s[6:7]
	s_waitcnt vmcnt(12)
	v_mul_f32_e32 v144, v26, v144
	v_mul_f32_e32 v145, v26, v145
	v_mul_f32_e32 v146, v26, v146
	v_mul_f32_e32 v147, v26, v147
	ds_write_b128 v209, v[144:147]
	v_mul_f32_e32 v148, v27, v148
	v_mul_f32_e32 v149, v27, v149
	v_mul_f32_e32 v150, v27, v150
	v_mul_f32_e32 v151, v27, v151
	ds_write_b128 v209, v[148:151] offset:1024
	v_mul_f32_e32 v152, v28, v152
	v_mul_f32_e32 v153, v28, v153
	v_mul_f32_e32 v154, v28, v154
	v_mul_f32_e32 v155, v28, v155
	ds_write_b128 v209, v[152:155] offset:2048
	v_mul_f32_e32 v156, v29, v156
	v_mul_f32_e32 v157, v29, v157
	v_mul_f32_e32 v158, v29, v158
	v_mul_f32_e32 v159, v29, v159
	ds_write_b128 v209, v[156:159] offset:3072
	v_mul_f32_e32 v160, v30, v160
	v_mul_f32_e32 v161, v30, v161
	v_mul_f32_e32 v162, v30, v162
	v_mul_f32_e32 v163, v30, v163
	ds_write_b128 v209, v[160:163] offset:4096
	v_mul_f32_e32 v164, v31, v164
	v_mul_f32_e32 v165, v31, v165
	v_mul_f32_e32 v166, v31, v166
	v_mul_f32_e32 v167, v31, v167
	ds_write_b128 v209, v[164:167] offset:5120
	v_mul_f32_e32 v168, v32, v168
	v_mul_f32_e32 v169, v32, v169
	v_mul_f32_e32 v170, v32, v170
	v_mul_f32_e32 v171, v32, v171
	ds_write_b128 v209, v[168:171] offset:6144
	v_mul_f32_e32 v172, v33, v172
	v_mul_f32_e32 v173, v33, v173
	v_mul_f32_e32 v174, v33, v174
	v_mul_f32_e32 v175, v33, v175
	ds_write_b128 v209, v[172:175] offset:7168
	s_waitcnt lgkmcnt(0)
	s_barrier
; #define GAS __attribute__((address_space(1)))
; #define LAS __attribute__((address_space(3)))
; #define LDS_WAIT() asm volatile("s_waitcnt lgkmcnt(0)" ::: "memory")
; __device__ __forceinline__ unsigned pk4_fp8(float a, float b, float c, float d) {
;     a = fminf(fmaxf(a, -448.f), 448.f); b = fminf(fmaxf(b, -448.f), 448.f); c = fminf(fmaxf(c, -448.f), 448.f); d = fminf(fmaxf(d, -448.f), 448.f);
;     int w = __builtin_amdgcn_cvt_pk_fp8_f32(a, b, 0, false); w = __builtin_amdgcn_cvt_pk_fp8_f32(c, d, w, true); return (unsigned)w; }
;     const int pr = item >> 1, kb = 2 * (pr / nblk) + (item & 1), nb = pr % nblk, k0 = 64 * kb, n0 = 32 * nb;
;     const int nr = n0 + (lane & 31); const int sc = MAP == 1 ? src_col_in(nr) : nr;
;     float v[32];
; #pragma unroll
;     for (int i = 0; i < 32; ++i) v[i] = sc >= 0 ? W[(size_t)(k0 + 2 * i + (lane >> 5)) * Nsrc + sc] : 0.f;
; #pragma unroll
;     for (int i = 0; i < 32; ++i) { const int k = k0 + 2 * i + (lane >> 5); float x = v[i] * wscale; if (KS) x *= (k < ksplit ? ksA[k] : ksB[k - ksplit]); scr[(2 * i + (lane >> 5)) * 33 + (lane & 31)] = x; }
;     LDS_WAIT(); asm volatile("" ::: "memory");
;     const int c = lane & 7;
; #pragma unroll
;     for (int j = 0; j < 4; ++j) { const int n = (lane >> 3) + 8 * j; const LAS float* s = scr + (8 * c) * 33 + n;
;         const unsigned long long o = (unsigned long long)pg8::pk4_fp8(s[0 * 33], s[1 * 33], s[2 * 33], s[3 * 33]) | ((unsigned long long)pg8::pk4_fp8(s[4 * 33], s[5 * 33], s[6 * 33], s[7 * 33]) << 32);
;         *(GAS unsigned long long*)(WT + (size_t)(n0 + n) * K + k0 + 8 * c) = o; }
;     LDS_WAIT(); asm volatile("" ::: "memory");
	s_add_u32 s8, s30, 0xa000
	s_addc_u32 s9, s31, 0
	global_load_dwordx4 v[144:147], v74, s[8:9]
	s_add_u32 s8, s8, 0x20000
	s_addc_u32 s9, s9, 0
	global_load_dwordx4 v[148:151], v74, s[8:9]
	s_add_u32 s8, s8, 0x20000
	s_addc_u32 s9, s9, 0
	global_load_dwordx4 v[152:155], v74, s[8:9]
	s_add_u32 s8, s8, 0x20000
	s_addc_u32 s9, s9, 0
	global_load_dwordx4 v[156:159], v74, s[8:9]
	s_add_u32 s8, s8, 0x20000
	s_addc_u32 s9, s9, 0
	global_load_dwordx4 v[160:163], v74, s[8:9]
	s_add_u32 s8, s8, 0x20000
	s_addc_u32 s9, s9, 0
	global_load_dwordx4 v[164:167], v74, s[8:9]
	s_add_u32 s8, s8, 0x20000
	s_addc_u32 s9, s9, 0
	global_load_dwordx4 v[168:171], v74, s[8:9]
	s_add_u32 s8, s8, 0x20000
	s_addc_u32 s9, s9, 0
	global_load_dwordx4 v[172:175], v74, s[8:9]
	s_add_u32 s6, s32, 0x2000000
	s_addc_u32 s7, s33, 0
	ds_read_b32 v226, v211
	ds_read_b32 v227, v211 offset:512
	ds_read_b32 v228, v211 offset:1024
	ds_read_b32 v229, v211 offset:1536
	ds_read_b32 v230, v211 offset:2048
	ds_read_b32 v231, v211 offset:2560
	ds_read_b32 v232, v211 offset:3072
	ds_read_b32 v233, v211 offset:3584
	ds_read_b32 v234, v211 offset:4096
	ds_read_b32 v235, v211 offset:4608
	ds_read_b32 v236, v211 offset:5120
	ds_read_b32 v237, v211 offset:5632
	ds_read_b32 v238, v211 offset:6144
	ds_read_b32 v239, v211 offset:6656
	ds_read_b32 v240, v211 offset:7168
	ds_read_b32 v241, v211 offset:7680
	s_waitcnt lgkmcnt(0)
	v_max_f32_e32 v226, v226, v226
	v_max_f32_e32 v227, v227, v227
	v_max_f32_e32 v228, v228, v228
	v_max_f32_e32 v229, v229, v229
	v_max_f32_e32 v230, v230, v230
	v_max_f32_e32 v231, v231, v231
	v_max_f32_e32 v232, v232, v232
	v_max_f32_e32 v233, v233, v233
	v_max_f32_e32 v234, v234, v234
	v_max_f32_e32 v235, v235, v235
	v_max_f32_e32 v236, v236, v236
	v_max_f32_e32 v237, v237, v237
	v_max_f32_e32 v238, v238, v238
	v_max_f32_e32 v239, v239, v239
	v_max_f32_e32 v240, v240, v240
	v_max_f32_e32 v241, v241, v241
	v_med3_f32 v226, v226, s62, v95
	v_med3_f32 v227, v227, s62, v95
	v_med3_f32 v228, v228, s62, v95
	v_med3_f32 v229, v229, s62, v95
	v_med3_f32 v230, v230, s62, v95
	v_med3_f32 v231, v231, s62, v95
	v_med3_f32 v232, v232, s62, v95
	v_med3_f32 v233, v233, s62, v95
	v_med3_f32 v234, v234, s62, v95
	v_med3_f32 v235, v235, s62, v95
	v_med3_f32 v236, v236, s62, v95
	v_med3_f32 v237, v237, s62, v95
	v_med3_f32 v238, v238, s62, v95
	v_med3_f32 v239, v239, s62, v95
	v_med3_f32 v240, v240, s62, v95
	v_med3_f32 v241, v241, s62, v95
	v_mov_b32_e32 v242, 0
	v_mov_b32_e32 v243, 0
	v_mov_b32_e32 v244, 0
	v_mov_b32_e32 v245, 0
	v_cvt_pk_fp8_f32 v242, v226, v227
	v_cvt_pk_fp8_f32 v243, v230, v231
	v_cvt_pk_fp8_f32 v244, v234, v235
	v_cvt_pk_fp8_f32 v245, v238, v239
	v_cvt_pk_fp8_f32 v242, v228, v229 op_sel:[0,0,1]
	v_cvt_pk_fp8_f32 v243, v232, v233 op_sel:[0,0,1]
	v_cvt_pk_fp8_f32 v244, v236, v237 op_sel:[0,0,1]
	v_cvt_pk_fp8_f32 v245, v240, v241 op_sel:[0,0,1]
	s_nop 0
	global_store_dwordx4 v77, v[242:245], s[6:7]
	ds_read_b32 v226, v213
	ds_read_b32 v227, v213 offset:512
	ds_read_b32 v228, v213 offset:1024
	ds_read_b32 v229, v213 offset:1536
	ds_read_b32 v230, v213 offset:2048
	ds_read_b32 v231, v213 offset:2560
	ds_read_b32 v232, v213 offset:3072
	ds_read_b32 v233, v213 offset:3584
	ds_read_b32 v234, v213 offset:4096
	ds_read_b32 v235, v213 offset:4608
	ds_read_b32 v236, v213 offset:5120
	ds_read_b32 v237, v213 offset:5632
	ds_read_b32 v238, v213 offset:6144
	ds_read_b32 v239, v213 offset:6656
	ds_read_b32 v240, v213 offset:7168
	ds_read_b32 v241, v213 offset:7680
	s_waitcnt lgkmcnt(0)
	v_max_f32_e32 v226, v226, v226
	v_max_f32_e32 v227, v227, v227
	v_max_f32_e32 v228, v228, v228
	v_max_f32_e32 v229, v229, v229
	v_max_f32_e32 v230, v230, v230
	v_max_f32_e32 v231, v231, v231
	v_max_f32_e32 v232, v232, v232
	v_max_f32_e32 v233, v233, v233
	v_max_f32_e32 v234, v234, v234
	v_max_f32_e32 v235, v235, v235
	v_max_f32_e32 v236, v236, v236
	v_max_f32_e32 v237, v237, v237
	v_max_f32_e32 v238, v238, v238
	v_max_f32_e32 v239, v239, v239
	v_max_f32_e32 v240, v240, v240
	v_max_f32_e32 v241, v241, v241
	v_med3_f32 v226, v226, s62, v95
	v_med3_f32 v227, v227, s62, v95
	v_med3_f32 v228, v228, s62, v95
	v_med3_f32 v229, v229, s62, v95
	v_med3_f32 v230, v230, s62, v95
	v_med3_f32 v231, v231, s62, v95
	v_med3_f32 v232, v232, s62, v95
	v_med3_f32 v233, v233, s62, v95
	v_med3_f32 v234, v234, s62, v95
	v_med3_f32 v235, v235, s62, v95
	v_med3_f32 v236, v236, s62, v95
	v_med3_f32 v237, v237, s62, v95
	v_med3_f32 v238, v238, s62, v95
	v_med3_f32 v239, v239, s62, v95
	v_med3_f32 v240, v240, s62, v95
	v_med3_f32 v241, v241, s62, v95
	v_mov_b32_e32 v242, 0
	v_mov_b32_e32 v243, 0
	v_mov_b32_e32 v244, 0
	v_mov_b32_e32 v245, 0
	v_cvt_pk_fp8_f32 v242, v226, v227
	v_cvt_pk_fp8_f32 v243, v230, v231
	v_cvt_pk_fp8_f32 v244, v234, v235
	v_cvt_pk_fp8_f32 v245, v238, v239
	v_cvt_pk_fp8_f32 v242, v228, v229 op_sel:[0,0,1]
	v_cvt_pk_fp8_f32 v243, v232, v233 op_sel:[0,0,1]
	v_cvt_pk_fp8_f32 v244, v236, v237 op_sel:[0,0,1]
	v_cvt_pk_fp8_f32 v245, v240, v241 op_sel:[0,0,1]
	s_nop 0
	global_store_dwordx4 v78, v[242:245], s[6:7]
	s_waitcnt vmcnt(12)
	v_mul_f32_e32 v176, v26, v176
	v_mul_f32_e32 v177, v26, v177
	v_mul_f32_e32 v178, v26, v178
	v_mul_f32_e32 v179, v26, v179
	ds_write_b128 v210, v[176:179]
	v_mul_f32_e32 v180, v27, v180
	v_mul_f32_e32 v181, v27, v181
	v_mul_f32_e32 v182, v27, v182
	v_mul_f32_e32 v183, v27, v183
	ds_write_b128 v210, v[180:183] offset:1024
	v_mul_f32_e32 v184, v28, v184
	v_mul_f32_e32 v185, v28, v185
	v_mul_f32_e32 v186, v28, v186
	v_mul_f32_e32 v187, v28, v187
	ds_write_b128 v210, v[184:187] offset:2048
	v_mul_f32_e32 v188, v29, v188
	v_mul_f32_e32 v189, v29, v189
	v_mul_f32_e32 v190, v29, v190
	v_mul_f32_e32 v191, v29, v191
	ds_write_b128 v210, v[188:191] offset:3072
	v_mul_f32_e32 v192, v30, v192
	v_mul_f32_e32 v193, v30, v193
	v_mul_f32_e32 v194, v30, v194
	v_mul_f32_e32 v195, v30, v195
	ds_write_b128 v210, v[192:195] offset:4096
	v_mul_f32_e32 v196, v31, v196
	v_mul_f32_e32 v197, v31, v197
	v_mul_f32_e32 v198, v31, v198
	v_mul_f32_e32 v199, v31, v199
	ds_write_b128 v210, v[196:199] offset:5120
	v_mul_f32_e32 v200, v32, v200
	v_mul_f32_e32 v201, v32, v201
	v_mul_f32_e32 v202, v32, v202
	v_mul_f32_e32 v203, v32, v203
	ds_write_b128 v210, v[200:203] offset:6144
	v_mul_f32_e32 v204, v33, v204
	v_mul_f32_e32 v205, v33, v205
	v_mul_f32_e32 v206, v33, v206
	v_mul_f32_e32 v207, v33, v207
	ds_write_b128 v210, v[204:207] offset:7168
	s_waitcnt lgkmcnt(0)
	s_barrier
; #define GAS __attribute__((address_space(1)))
; #define LAS __attribute__((address_space(3)))
; #define LDS_WAIT() asm volatile("s_waitcnt lgkmcnt(0)" ::: "memory")
; __device__ __forceinline__ unsigned pk4_fp8(float a, float b, float c, float d) {
;     a = fminf(fmaxf(a, -448.f), 448.f); b = fminf(fmaxf(b, -448.f), 448.f); c = fminf(fmaxf(c, -448.f), 448.f); d = fminf(fmaxf(d, -448.f), 448.f);
;     int w = __builtin_amdgcn_cvt_pk_fp8_f32(a, b, 0, false); w = __builtin_amdgcn_cvt_pk_fp8_f32(c, d, w, true); return (unsigned)w; }
;     const int pr = item >> 1, kb = 2 * (pr / nblk) + (item & 1), nb = pr % nblk, k0 = 64 * kb, n0 = 32 * nb;
;     const int nr = n0 + (lane & 31); const int sc = MAP == 1 ? src_col_in(nr) : nr;
;     float v[32];
; #pragma unroll
;     for (int i = 0; i < 32; ++i) v[i] = sc >= 0 ? W[(size_t)(k0 + 2 * i + (lane >> 5)) * Nsrc + sc] : 0.f;
; #pragma unroll
;     for (int i = 0; i < 32; ++i) { const int k = k0 + 2 * i + (lane >> 5); float x = v[i] * wscale; if (KS) x *= (k < ksplit ? ksA[k] : ksB[k - ksplit]); scr[(2 * i + (lane >> 5)) * 33 + (lane & 31)] = x; }
;     LDS_WAIT(); asm volatile("" ::: "memory");
;     const int c = lane & 7;
; #pragma unroll
;     for (int j = 0; j < 4; ++j) { const int n = (lane >> 3) + 8 * j; const LAS float* s = scr + (8 * c) * 33 + n;
;         const unsigned long long o = (unsigned long long)pg8::pk4_fp8(s[0 * 33], s[1 * 33], s[2 * 33], s[3 * 33]) | ((unsigned long long)pg8::pk4_fp8(s[4 * 33], s[5 * 33], s[6 * 33], s[7 * 33]) << 32);
;         *(GAS unsigned long long*)(WT + (size_t)(n0 + n) * K + k0 + 8 * c) = o; }
;     LDS_WAIT(); asm volatile("" ::: "memory");
; }
	s_add_u32 s8, s30, 0xb000
	s_addc_u32 s9, s31, 0
	global_load_dwordx4 v[176:179], v74, s[8:9]
	s_add_u32 s8, s8, 0x20000
	s_addc_u32 s9, s9, 0
	global_load_dwordx4 v[180:183], v74, s[8:9]
	s_add_u32 s8, s8, 0x20000
	s_addc_u32 s9, s9, 0
	global_load_dwordx4 v[184:187], v74, s[8:9]
	s_add_u32 s8, s8, 0x20000
	s_addc_u32 s9, s9, 0
	global_load_dwordx4 v[188:191], v74, s[8:9]
	s_add_u32 s8, s8, 0x20000
	s_addc_u32 s9, s9, 0
	global_load_dwordx4 v[192:195], v74, s[8:9]
	s_add_u32 s8, s8, 0x20000
	s_addc_u32 s9, s9, 0
	global_load_dwordx4 v[196:199], v74, s[8:9]
	s_add_u32 s8, s8, 0x20000
	s_addc_u32 s9, s9, 0
	global_load_dwordx4 v[200:203], v74, s[8:9]
	s_add_u32 s8, s8, 0x20000
	s_addc_u32 s9, s9, 0
	global_load_dwordx4 v[204:207], v74, s[8:9]
	s_add_u32 s6, s32, 0x2400000
	s_addc_u32 s7, s33, 0
	ds_read_b32 v226, v212
	ds_read_b32 v227, v212 offset:512
	ds_read_b32 v228, v212 offset:1024
	ds_read_b32 v229, v212 offset:1536
	ds_read_b32 v230, v212 offset:2048
	ds_read_b32 v231, v212 offset:2560
	ds_read_b32 v232, v212 offset:3072
	ds_read_b32 v233, v212 offset:3584
	ds_read_b32 v234, v212 offset:4096
	ds_read_b32 v235, v212 offset:4608
	ds_read_b32 v236, v212 offset:5120
	ds_read_b32 v237, v212 offset:5632
	ds_read_b32 v238, v212 offset:6144
	ds_read_b32 v239, v212 offset:6656
	ds_read_b32 v240, v212 offset:7168
	ds_read_b32 v241, v212 offset:7680
	s_waitcnt lgkmcnt(0)
	v_max_f32_e32 v226, v226, v226
	v_max_f32_e32 v227, v227, v227
	v_max_f32_e32 v228, v228, v228
	v_max_f32_e32 v229, v229, v229
	v_max_f32_e32 v230, v230, v230
	v_max_f32_e32 v231, v231, v231
	v_max_f32_e32 v232, v232, v232
	v_max_f32_e32 v233, v233, v233
	v_max_f32_e32 v234, v234, v234
	v_max_f32_e32 v235, v235, v235
	v_max_f32_e32 v236, v236, v236
	v_max_f32_e32 v237, v237, v237
	v_max_f32_e32 v238, v238, v238
	v_max_f32_e32 v239, v239, v239
	v_max_f32_e32 v240, v240, v240
	v_max_f32_e32 v241, v241, v241
	v_med3_f32 v226, v226, s62, v95
	v_med3_f32 v227, v227, s62, v95
	v_med3_f32 v228, v228, s62, v95
	v_med3_f32 v229, v229, s62, v95
	v_med3_f32 v230, v230, s62, v95
	v_med3_f32 v231, v231, s62, v95
	v_med3_f32 v232, v232, s62, v95
	v_med3_f32 v233, v233, s62, v95
	v_med3_f32 v234, v234, s62, v95
	v_med3_f32 v235, v235, s62, v95
	v_med3_f32 v236, v236, s62, v95
	v_med3_f32 v237, v237, s62, v95
	v_med3_f32 v238, v238, s62, v95
	v_med3_f32 v239, v239, s62, v95
	v_med3_f32 v240, v240, s62, v95
	v_med3_f32 v241, v241, s62, v95
	v_mov_b32_e32 v242, 0
	v_mov_b32_e32 v243, 0
	v_mov_b32_e32 v244, 0
	v_mov_b32_e32 v245, 0
	v_cvt_pk_fp8_f32 v242, v226, v227
	v_cvt_pk_fp8_f32 v243, v230, v231
	v_cvt_pk_fp8_f32 v244, v234, v235
	v_cvt_pk_fp8_f32 v245, v238, v239
	v_cvt_pk_fp8_f32 v242, v228, v229 op_sel:[0,0,1]
	v_cvt_pk_fp8_f32 v243, v232, v233 op_sel:[0,0,1]
	v_cvt_pk_fp8_f32 v244, v236, v237 op_sel:[0,0,1]
	v_cvt_pk_fp8_f32 v245, v240, v241 op_sel:[0,0,1]
	s_nop 0
	global_store_dwordx4 v77, v[242:245], s[6:7]
	ds_read_b32 v226, v214
	ds_read_b32 v227, v214 offset:512
	ds_read_b32 v228, v214 offset:1024
	ds_read_b32 v229, v214 offset:1536
	ds_read_b32 v230, v214 offset:2048
	ds_read_b32 v231, v214 offset:2560
	ds_read_b32 v232, v214 offset:3072
	ds_read_b32 v233, v214 offset:3584
	ds_read_b32 v234, v214 offset:4096
	ds_read_b32 v235, v214 offset:4608
	ds_read_b32 v236, v214 offset:5120
	ds_read_b32 v237, v214 offset:5632
	ds_read_b32 v238, v214 offset:6144
	ds_read_b32 v239, v214 offset:6656
	ds_read_b32 v240, v214 offset:7168
	ds_read_b32 v241, v214 offset:7680
	s_waitcnt lgkmcnt(0)
	v_max_f32_e32 v226, v226, v226
	v_max_f32_e32 v227, v227, v227
	v_max_f32_e32 v228, v228, v228
	v_max_f32_e32 v229, v229, v229
	v_max_f32_e32 v230, v230, v230
	v_max_f32_e32 v231, v231, v231
	v_max_f32_e32 v232, v232, v232
	v_max_f32_e32 v233, v233, v233
	v_max_f32_e32 v234, v234, v234
	v_max_f32_e32 v235, v235, v235
	v_max_f32_e32 v236, v236, v236
	v_max_f32_e32 v237, v237, v237
	v_max_f32_e32 v238, v238, v238
	v_max_f32_e32 v239, v239, v239
	v_max_f32_e32 v240, v240, v240
	v_max_f32_e32 v241, v241, v241
	v_med3_f32 v226, v226, s62, v95
	v_med3_f32 v227, v227, s62, v95
	v_med3_f32 v228, v228, s62, v95
	v_med3_f32 v229, v229, s62, v95
	v_med3_f32 v230, v230, s62, v95
	v_med3_f32 v231, v231, s62, v95
	v_med3_f32 v232, v232, s62, v95
	v_med3_f32 v233, v233, s62, v95
	v_med3_f32 v234, v234, s62, v95
	v_med3_f32 v235, v235, s62, v95
	v_med3_f32 v236, v236, s62, v95
	v_med3_f32 v237, v237, s62, v95
	v_med3_f32 v238, v238, s62, v95
	v_med3_f32 v239, v239, s62, v95
	v_med3_f32 v240, v240, s62, v95
	v_med3_f32 v241, v241, s62, v95
	v_mov_b32_e32 v242, 0
	v_mov_b32_e32 v243, 0
	v_mov_b32_e32 v244, 0
	v_mov_b32_e32 v245, 0
	v_cvt_pk_fp8_f32 v242, v226, v227
	v_cvt_pk_fp8_f32 v243, v230, v231
	v_cvt_pk_fp8_f32 v244, v234, v235
	v_cvt_pk_fp8_f32 v245, v238, v239
	v_cvt_pk_fp8_f32 v242, v228, v229 op_sel:[0,0,1]
	v_cvt_pk_fp8_f32 v243, v232, v233 op_sel:[0,0,1]
	v_cvt_pk_fp8_f32 v244, v236, v237 op_sel:[0,0,1]
	v_cvt_pk_fp8_f32 v245, v240, v241 op_sel:[0,0,1]
	s_nop 0
	global_store_dwordx4 v78, v[242:245], s[6:7]
	s_waitcnt vmcnt(12)
	v_mul_f32_e32 v144, v26, v144
	v_mul_f32_e32 v145, v26, v145
	v_mul_f32_e32 v146, v26, v146
	v_mul_f32_e32 v147, v26, v147
	ds_write_b128 v209, v[144:147]
	v_mul_f32_e32 v148, v27, v148
	v_mul_f32_e32 v149, v27, v149
	v_mul_f32_e32 v150, v27, v150
	v_mul_f32_e32 v151, v27, v151
	ds_write_b128 v209, v[148:151] offset:1024
	v_mul_f32_e32 v152, v28, v152
	v_mul_f32_e32 v153, v28, v153
	v_mul_f32_e32 v154, v28, v154
	v_mul_f32_e32 v155, v28, v155
	ds_write_b128 v209, v[152:155] offset:2048
	v_mul_f32_e32 v156, v29, v156
	v_mul_f32_e32 v157, v29, v157
	v_mul_f32_e32 v158, v29, v158
	v_mul_f32_e32 v159, v29, v159
	ds_write_b128 v209, v[156:159] offset:3072
	v_mul_f32_e32 v160, v30, v160
	v_mul_f32_e32 v161, v30, v161
	v_mul_f32_e32 v162, v30, v162
	v_mul_f32_e32 v163, v30, v163
	ds_write_b128 v209, v[160:163] offset:4096
	v_mul_f32_e32 v164, v31, v164
	v_mul_f32_e32 v165, v31, v165
	v_mul_f32_e32 v166, v31, v166
	v_mul_f32_e32 v167, v31, v167
	ds_write_b128 v209, v[164:167] offset:5120
	v_mul_f32_e32 v168, v32, v168
	v_mul_f32_e32 v169, v32, v169
	v_mul_f32_e32 v170, v32, v170
	v_mul_f32_e32 v171, v32, v171
	ds_write_b128 v209, v[168:171] offset:6144
	v_mul_f32_e32 v172, v33, v172
	v_mul_f32_e32 v173, v33, v173
	v_mul_f32_e32 v174, v33, v174
	v_mul_f32_e32 v175, v33, v175
	ds_write_b128 v209, v[172:175] offset:7168
	s_waitcnt lgkmcnt(0)
	s_barrier
; #define GAS __attribute__((address_space(1)))
; #define LAS __attribute__((address_space(3)))
; #define LDS_WAIT() asm volatile("s_waitcnt lgkmcnt(0)" ::: "memory")
; __device__ __forceinline__ unsigned pk4_fp8(float a, float b, float c, float d) {
;     a = fminf(fmaxf(a, -448.f), 448.f); b = fminf(fmaxf(b, -448.f), 448.f); c = fminf(fmaxf(c, -448.f), 448.f); d = fminf(fmaxf(d, -448.f), 448.f);
;     int w = __builtin_amdgcn_cvt_pk_fp8_f32(a, b, 0, false); w = __builtin_amdgcn_cvt_pk_fp8_f32(c, d, w, true); return (unsigned)w; }
;     const int pr = item >> 1, kb = 2 * (pr / nblk) + (item & 1), nb = pr % nblk, k0 = 64 * kb, n0 = 32 * nb;
;     const int nr = n0 + (lane & 31); const int sc = MAP == 1 ? src_col_in(nr) : nr;
;     float v[32];
; #pragma unroll
;     for (int i = 0; i < 32; ++i) v[i] = sc >= 0 ? W[(size_t)(k0 + 2 * i + (lane >> 5)) * Nsrc + sc] : 0.f;
; #pragma unroll
;     for (int i = 0; i < 32; ++i) { const int k = k0 + 2 * i + (lane >> 5); float x = v[i] * wscale; if (KS) x *= (k < ksplit ? ksA[k] : ksB[k - ksplit]); scr[(2 * i + (lane >> 5)) * 33 + (lane & 31)] = x; }
;     LDS_WAIT(); asm volatile("" ::: "memory");
;     const int c = lane & 7;
; #pragma unroll
;     for (int j = 0; j < 4; ++j) { const int n = (lane >> 3) + 8 * j; const LAS float* s = scr + (8 * c) * 33 + n;
;         const unsigned long long o = (unsigned long long)pg8::pk4_fp8(s[0 * 33], s[1 * 33], s[2 * 33], s[3 * 33]) | ((unsigned long long)pg8::pk4_fp8(s[4 * 33], s[5 * 33], s[6 * 33], s[7 * 33]) << 32);
;         *(GAS unsigned long long*)(WT + (size_t)(n0 + n) * K + k0 + 8 * c) = o; }
;     LDS_WAIT(); asm volatile("" ::: "memory");
; }
	s_add_u32 s8, s30, 0xc000
	s_addc_u32 s9, s31, 0
	global_load_dwordx4 v[144:147], v74, s[8:9]
	s_add_u32 s8, s8, 0x20000
	s_addc_u32 s9, s9, 0
	global_load_dwordx4 v[148:151], v74, s[8:9]
	s_add_u32 s8, s8, 0x20000
	s_addc_u32 s9, s9, 0
	global_load_dwordx4 v[152:155], v74, s[8:9]
	s_add_u32 s8, s8, 0x20000
	s_addc_u32 s9, s9, 0
	global_load_dwordx4 v[156:159], v74, s[8:9]
	s_add_u32 s8, s8, 0x20000
	s_addc_u32 s9, s9, 0
	global_load_dwordx4 v[160:163], v74, s[8:9]
	s_add_u32 s8, s8, 0x20000
	s_addc_u32 s9, s9, 0
	global_load_dwordx4 v[164:167], v74, s[8:9]
	s_add_u32 s8, s8, 0x20000
	s_addc_u32 s9, s9, 0
	global_load_dwordx4 v[168:171], v74, s[8:9]
	s_add_u32 s8, s8, 0x20000
	s_addc_u32 s9, s9, 0
	global_load_dwordx4 v[172:175], v74, s[8:9]
	s_add_u32 s6, s32, 0x2800000
	s_addc_u32 s7, s33, 0
	ds_read_b32 v226, v211
	ds_read_b32 v227, v211 offset:512
	ds_read_b32 v228, v211 offset:1024
	ds_read_b32 v229, v211 offset:1536
	ds_read_b32 v230, v211 offset:2048
	ds_read_b32 v231, v211 offset:2560
	ds_read_b32 v232, v211 offset:3072
	ds_read_b32 v233, v211 offset:3584
	ds_read_b32 v234, v211 offset:4096
	ds_read_b32 v235, v211 offset:4608
	ds_read_b32 v236, v211 offset:5120
	ds_read_b32 v237, v211 offset:5632
	ds_read_b32 v238, v211 offset:6144
	ds_read_b32 v239, v211 offset:6656
	ds_read_b32 v240, v211 offset:7168
	ds_read_b32 v241, v211 offset:7680
	s_waitcnt lgkmcnt(0)
	v_max_f32_e32 v226, v226, v226
	v_max_f32_e32 v227, v227, v227
	v_max_f32_e32 v228, v228, v228
	v_max_f32_e32 v229, v229, v229
	v_max_f32_e32 v230, v230, v230
	v_max_f32_e32 v231, v231, v231
	v_max_f32_e32 v232, v232, v232
	v_max_f32_e32 v233, v233, v233
	v_max_f32_e32 v234, v234, v234
	v_max_f32_e32 v235, v235, v235
	v_max_f32_e32 v236, v236, v236
	v_max_f32_e32 v237, v237, v237
	v_max_f32_e32 v238, v238, v238
	v_max_f32_e32 v239, v239, v239
	v_max_f32_e32 v240, v240, v240
	v_max_f32_e32 v241, v241, v241
	v_med3_f32 v226, v226, s62, v95
	v_med3_f32 v227, v227, s62, v95
	v_med3_f32 v228, v228, s62, v95
	v_med3_f32 v229, v229, s62, v95
	v_med3_f32 v230, v230, s62, v95
	v_med3_f32 v231, v231, s62, v95
	v_med3_f32 v232, v232, s62, v95
	v_med3_f32 v233, v233, s62, v95
	v_med3_f32 v234, v234, s62, v95
	v_med3_f32 v235, v235, s62, v95
	v_med3_f32 v236, v236, s62, v95
	v_med3_f32 v237, v237, s62, v95
	v_med3_f32 v238, v238, s62, v95
	v_med3_f32 v239, v239, s62, v95
	v_med3_f32 v240, v240, s62, v95
	v_med3_f32 v241, v241, s62, v95
	v_mov_b32_e32 v242, 0
	v_mov_b32_e32 v243, 0
	v_mov_b32_e32 v244, 0
	v_mov_b32_e32 v245, 0
	v_cvt_pk_fp8_f32 v242, v226, v227
	v_cvt_pk_fp8_f32 v243, v230, v231
	v_cvt_pk_fp8_f32 v244, v234, v235
	v_cvt_pk_fp8_f32 v245, v238, v239
	v_cvt_pk_fp8_f32 v242, v228, v229 op_sel:[0,0,1]
	v_cvt_pk_fp8_f32 v243, v232, v233 op_sel:[0,0,1]
	v_cvt_pk_fp8_f32 v244, v236, v237 op_sel:[0,0,1]
	v_cvt_pk_fp8_f32 v245, v240, v241 op_sel:[0,0,1]
	s_nop 0
	global_store_dwordx4 v77, v[242:245], s[6:7]
	ds_read_b32 v226, v213
	ds_read_b32 v227, v213 offset:512
	ds_read_b32 v228, v213 offset:1024
	ds_read_b32 v229, v213 offset:1536
	ds_read_b32 v230, v213 offset:2048
	ds_read_b32 v231, v213 offset:2560
	ds_read_b32 v232, v213 offset:3072
	ds_read_b32 v233, v213 offset:3584
	ds_read_b32 v234, v213 offset:4096
	ds_read_b32 v235, v213 offset:4608
	ds_read_b32 v236, v213 offset:5120
	ds_read_b32 v237, v213 offset:5632
	ds_read_b32 v238, v213 offset:6144
	ds_read_b32 v239, v213 offset:6656
	ds_read_b32 v240, v213 offset:7168
	ds_read_b32 v241, v213 offset:7680
	s_waitcnt lgkmcnt(0)
	v_max_f32_e32 v226, v226, v226
	v_max_f32_e32 v227, v227, v227
	v_max_f32_e32 v228, v228, v228
	v_max_f32_e32 v229, v229, v229
	v_max_f32_e32 v230, v230, v230
	v_max_f32_e32 v231, v231, v231
	v_max_f32_e32 v232, v232, v232
	v_max_f32_e32 v233, v233, v233
	v_max_f32_e32 v234, v234, v234
	v_max_f32_e32 v235, v235, v235
	v_max_f32_e32 v236, v236, v236
	v_max_f32_e32 v237, v237, v237
	v_max_f32_e32 v238, v238, v238
	v_max_f32_e32 v239, v239, v239
	v_max_f32_e32 v240, v240, v240
	v_max_f32_e32 v241, v241, v241
	v_med3_f32 v226, v226, s62, v95
	v_med3_f32 v227, v227, s62, v95
	v_med3_f32 v228, v228, s62, v95
	v_med3_f32 v229, v229, s62, v95
	v_med3_f32 v230, v230, s62, v95
	v_med3_f32 v231, v231, s62, v95
	v_med3_f32 v232, v232, s62, v95
	v_med3_f32 v233, v233, s62, v95
	v_med3_f32 v234, v234, s62, v95
	v_med3_f32 v235, v235, s62, v95
	v_med3_f32 v236, v236, s62, v95
	v_med3_f32 v237, v237, s62, v95
	v_med3_f32 v238, v238, s62, v95
	v_med3_f32 v239, v239, s62, v95
	v_med3_f32 v240, v240, s62, v95
	v_med3_f32 v241, v241, s62, v95
	v_mov_b32_e32 v242, 0
	v_mov_b32_e32 v243, 0
	v_mov_b32_e32 v244, 0
	v_mov_b32_e32 v245, 0
	v_cvt_pk_fp8_f32 v242, v226, v227
	v_cvt_pk_fp8_f32 v243, v230, v231
	v_cvt_pk_fp8_f32 v244, v234, v235
	v_cvt_pk_fp8_f32 v245, v238, v239
	v_cvt_pk_fp8_f32 v242, v228, v229 op_sel:[0,0,1]
	v_cvt_pk_fp8_f32 v243, v232, v233 op_sel:[0,0,1]
	v_cvt_pk_fp8_f32 v244, v236, v237 op_sel:[0,0,1]
	v_cvt_pk_fp8_f32 v245, v240, v241 op_sel:[0,0,1]
	s_nop 0
	global_store_dwordx4 v78, v[242:245], s[6:7]
	s_waitcnt vmcnt(12)
	v_mul_f32_e32 v176, v26, v176
	v_mul_f32_e32 v177, v26, v177
	v_mul_f32_e32 v178, v26, v178
	v_mul_f32_e32 v179, v26, v179
	ds_write_b128 v210, v[176:179]
	v_mul_f32_e32 v180, v27, v180
	v_mul_f32_e32 v181, v27, v181
	v_mul_f32_e32 v182, v27, v182
	v_mul_f32_e32 v183, v27, v183
	ds_write_b128 v210, v[180:183] offset:1024
	v_mul_f32_e32 v184, v28, v184
	v_mul_f32_e32 v185, v28, v185
	v_mul_f32_e32 v186, v28, v186
	v_mul_f32_e32 v187, v28, v187
	ds_write_b128 v210, v[184:187] offset:2048
	v_mul_f32_e32 v188, v29, v188
	v_mul_f32_e32 v189, v29, v189
	v_mul_f32_e32 v190, v29, v190
	v_mul_f32_e32 v191, v29, v191
	ds_write_b128 v210, v[188:191] offset:3072
	v_mul_f32_e32 v192, v30, v192
	v_mul_f32_e32 v193, v30, v193
	v_mul_f32_e32 v194, v30, v194
	v_mul_f32_e32 v195, v30, v195
	ds_write_b128 v210, v[192:195] offset:4096
	v_mul_f32_e32 v196, v31, v196
	v_mul_f32_e32 v197, v31, v197
	v_mul_f32_e32 v198, v31, v198
	v_mul_f32_e32 v199, v31, v199
	ds_write_b128 v210, v[196:199] offset:5120
	v_mul_f32_e32 v200, v32, v200
	v_mul_f32_e32 v201, v32, v201
	v_mul_f32_e32 v202, v32, v202
	v_mul_f32_e32 v203, v32, v203
	ds_write_b128 v210, v[200:203] offset:6144
	v_mul_f32_e32 v204, v33, v204
	v_mul_f32_e32 v205, v33, v205
	v_mul_f32_e32 v206, v33, v206
	v_mul_f32_e32 v207, v33, v207
	ds_write_b128 v210, v[204:207] offset:7168
	s_waitcnt lgkmcnt(0)
	s_barrier
; #define GAS __attribute__((address_space(1)))
; #define LAS __attribute__((address_space(3)))
; #define LDS_WAIT() asm volatile("s_waitcnt lgkmcnt(0)" ::: "memory")
; __device__ __forceinline__ unsigned pk4_fp8(float a, float b, float c, float d) {
;     a = fminf(fmaxf(a, -448.f), 448.f); b = fminf(fmaxf(b, -448.f), 448.f); c = fminf(fmaxf(c, -448.f), 448.f); d = fminf(fmaxf(d, -448.f), 448.f);
;     int w = __builtin_amdgcn_cvt_pk_fp8_f32(a, b, 0, false); w = __builtin_amdgcn_cvt_pk_fp8_f32(c, d, w, true); return (unsigned)w; }
;     const int pr = item >> 1, kb = 2 * (pr / nblk) + (item & 1), nb = pr % nblk, k0 = 64 * kb, n0 = 32 * nb;
;     const int nr = n0 + (lane & 31); const int sc = MAP == 1 ? src_col_in(nr) : nr;
;     float v[32];
; #pragma unroll
;     for (int i = 0; i < 32; ++i) v[i] = sc >= 0 ? W[(size_t)(k0 + 2 * i + (lane >> 5)) * Nsrc + sc] : 0.f;
; #pragma unroll
;     for (int i = 0; i < 32; ++i) { const int k = k0 + 2 * i + (lane >> 5); float x = v[i] * wscale; if (KS) x *= (k < ksplit ? ksA[k] : ksB[k - ksplit]); scr[(2 * i + (lane >> 5)) * 33 + (lane & 31)] = x; }
;     LDS_WAIT(); asm volatile("" ::: "memory");
;     const int c = lane & 7;
; #pragma unroll
;     for (int j = 0; j < 4; ++j) { const int n = (lane >> 3) + 8 * j; const LAS float* s = scr + (8 * c) * 33 + n;
;         const unsigned long long o = (unsigned long long)pg8::pk4_fp8(s[0 * 33], s[1 * 33], s[2 * 33], s[3 * 33]) | ((unsigned long long)pg8::pk4_fp8(s[4 * 33], s[5 * 33], s[6 * 33], s[7 * 33]) << 32);
;         *(GAS unsigned long long*)(WT + (size_t)(n0 + n) * K + k0 + 8 * c) = o; }
;     LDS_WAIT(); asm volatile("" ::: "memory");
; }
	s_add_u32 s8, s30, 0xd000
	s_addc_u32 s9, s31, 0
	global_load_dwordx4 v[176:179], v74, s[8:9]
	s_add_u32 s8, s8, 0x20000
	s_addc_u32 s9, s9, 0
	global_load_dwordx4 v[180:183], v74, s[8:9]
	s_add_u32 s8, s8, 0x20000
	s_addc_u32 s9, s9, 0
	global_load_dwordx4 v[184:187], v74, s[8:9]
	s_add_u32 s8, s8, 0x20000
	s_addc_u32 s9, s9, 0
	global_load_dwordx4 v[188:191], v74, s[8:9]
	s_add_u32 s8, s8, 0x20000
	s_addc_u32 s9, s9, 0
	global_load_dwordx4 v[192:195], v74, s[8:9]
	s_add_u32 s8, s8, 0x20000
	s_addc_u32 s9, s9, 0
	global_load_dwordx4 v[196:199], v74, s[8:9]
	s_add_u32 s8, s8, 0x20000
	s_addc_u32 s9, s9, 0
	global_load_dwordx4 v[200:203], v74, s[8:9]
	s_add_u32 s8, s8, 0x20000
	s_addc_u32 s9, s9, 0
	global_load_dwordx4 v[204:207], v74, s[8:9]
	s_add_u32 s6, s32, 0x2c00000
	s_addc_u32 s7, s33, 0
	ds_read_b32 v226, v212
	ds_read_b32 v227, v212 offset:512
	ds_read_b32 v228, v212 offset:1024
	ds_read_b32 v229, v212 offset:1536
	ds_read_b32 v230, v212 offset:2048
	ds_read_b32 v231, v212 offset:2560
	ds_read_b32 v232, v212 offset:3072
	ds_read_b32 v233, v212 offset:3584
	ds_read_b32 v234, v212 offset:4096
	ds_read_b32 v235, v212 offset:4608
	ds_read_b32 v236, v212 offset:5120
	ds_read_b32 v237, v212 offset:5632
	ds_read_b32 v238, v212 offset:6144
	ds_read_b32 v239, v212 offset:6656
	ds_read_b32 v240, v212 offset:7168
	ds_read_b32 v241, v212 offset:7680
	s_waitcnt lgkmcnt(0)
	v_max_f32_e32 v226, v226, v226
	v_max_f32_e32 v227, v227, v227
	v_max_f32_e32 v228, v228, v228
	v_max_f32_e32 v229, v229, v229
	v_max_f32_e32 v230, v230, v230
	v_max_f32_e32 v231, v231, v231
	v_max_f32_e32 v232, v232, v232
	v_max_f32_e32 v233, v233, v233
	v_max_f32_e32 v234, v234, v234
	v_max_f32_e32 v235, v235, v235
	v_max_f32_e32 v236, v236, v236
	v_max_f32_e32 v237, v237, v237
	v_max_f32_e32 v238, v238, v238
	v_max_f32_e32 v239, v239, v239
	v_max_f32_e32 v240, v240, v240
	v_max_f32_e32 v241, v241, v241
	v_med3_f32 v226, v226, s62, v95
	v_med3_f32 v227, v227, s62, v95
	v_med3_f32 v228, v228, s62, v95
	v_med3_f32 v229, v229, s62, v95
	v_med3_f32 v230, v230, s62, v95
	v_med3_f32 v231, v231, s62, v95
	v_med3_f32 v232, v232, s62, v95
	v_med3_f32 v233, v233, s62, v95
	v_med3_f32 v234, v234, s62, v95
	v_med3_f32 v235, v235, s62, v95
	v_med3_f32 v236, v236, s62, v95
	v_med3_f32 v237, v237, s62, v95
	v_med3_f32 v238, v238, s62, v95
	v_med3_f32 v239, v239, s62, v95
	v_med3_f32 v240, v240, s62, v95
	v_med3_f32 v241, v241, s62, v95
	v_mov_b32_e32 v242, 0
	v_mov_b32_e32 v243, 0
	v_mov_b32_e32 v244, 0
	v_mov_b32_e32 v245, 0
	v_cvt_pk_fp8_f32 v242, v226, v227
	v_cvt_pk_fp8_f32 v243, v230, v231
	v_cvt_pk_fp8_f32 v244, v234, v235
	v_cvt_pk_fp8_f32 v245, v238, v239
	v_cvt_pk_fp8_f32 v242, v228, v229 op_sel:[0,0,1]
	v_cvt_pk_fp8_f32 v243, v232, v233 op_sel:[0,0,1]
	v_cvt_pk_fp8_f32 v244, v236, v237 op_sel:[0,0,1]
	v_cvt_pk_fp8_f32 v245, v240, v241 op_sel:[0,0,1]
	s_nop 0
	global_store_dwordx4 v77, v[242:245], s[6:7]
	ds_read_b32 v226, v214
	ds_read_b32 v227, v214 offset:512
	ds_read_b32 v228, v214 offset:1024
	ds_read_b32 v229, v214 offset:1536
	ds_read_b32 v230, v214 offset:2048
	ds_read_b32 v231, v214 offset:2560
	ds_read_b32 v232, v214 offset:3072
	ds_read_b32 v233, v214 offset:3584
	ds_read_b32 v234, v214 offset:4096
	ds_read_b32 v235, v214 offset:4608
	ds_read_b32 v236, v214 offset:5120
	ds_read_b32 v237, v214 offset:5632
	ds_read_b32 v238, v214 offset:6144
	ds_read_b32 v239, v214 offset:6656
	ds_read_b32 v240, v214 offset:7168
	ds_read_b32 v241, v214 offset:7680
	s_waitcnt lgkmcnt(0)
	v_max_f32_e32 v226, v226, v226
	v_max_f32_e32 v227, v227, v227
	v_max_f32_e32 v228, v228, v228
	v_max_f32_e32 v229, v229, v229
	v_max_f32_e32 v230, v230, v230
	v_max_f32_e32 v231, v231, v231
	v_max_f32_e32 v232, v232, v232
	v_max_f32_e32 v233, v233, v233
	v_max_f32_e32 v234, v234, v234
	v_max_f32_e32 v235, v235, v235
	v_max_f32_e32 v236, v236, v236
	v_max_f32_e32 v237, v237, v237
	v_max_f32_e32 v238, v238, v238
	v_max_f32_e32 v239, v239, v239
	v_max_f32_e32 v240, v240, v240
	v_max_f32_e32 v241, v241, v241
	v_med3_f32 v226, v226, s62, v95
	v_med3_f32 v227, v227, s62, v95
	v_med3_f32 v228, v228, s62, v95
	v_med3_f32 v229, v229, s62, v95
	v_med3_f32 v230, v230, s62, v95
	v_med3_f32 v231, v231, s62, v95
	v_med3_f32 v232, v232, s62, v95
	v_med3_f32 v233, v233, s62, v95
	v_med3_f32 v234, v234, s62, v95
	v_med3_f32 v235, v235, s62, v95
	v_med3_f32 v236, v236, s62, v95
	v_med3_f32 v237, v237, s62, v95
	v_med3_f32 v238, v238, s62, v95
	v_med3_f32 v239, v239, s62, v95
	v_med3_f32 v240, v240, s62, v95
	v_med3_f32 v241, v241, s62, v95
	v_mov_b32_e32 v242, 0
	v_mov_b32_e32 v243, 0
	v_mov_b32_e32 v244, 0
	v_mov_b32_e32 v245, 0
	v_cvt_pk_fp8_f32 v242, v226, v227
	v_cvt_pk_fp8_f32 v243, v230, v231
	v_cvt_pk_fp8_f32 v244, v234, v235
	v_cvt_pk_fp8_f32 v245, v238, v239
	v_cvt_pk_fp8_f32 v242, v228, v229 op_sel:[0,0,1]
	v_cvt_pk_fp8_f32 v243, v232, v233 op_sel:[0,0,1]
	v_cvt_pk_fp8_f32 v244, v236, v237 op_sel:[0,0,1]
	v_cvt_pk_fp8_f32 v245, v240, v241 op_sel:[0,0,1]
	s_nop 0
	global_store_dwordx4 v78, v[242:245], s[6:7]
	s_waitcnt vmcnt(12)
	v_mul_f32_e32 v144, v26, v144
	v_mul_f32_e32 v145, v26, v145
	v_mul_f32_e32 v146, v26, v146
	v_mul_f32_e32 v147, v26, v147
	ds_write_b128 v209, v[144:147]
	v_mul_f32_e32 v148, v27, v148
	v_mul_f32_e32 v149, v27, v149
	v_mul_f32_e32 v150, v27, v150
	v_mul_f32_e32 v151, v27, v151
	ds_write_b128 v209, v[148:151] offset:1024
	v_mul_f32_e32 v152, v28, v152
	v_mul_f32_e32 v153, v28, v153
	v_mul_f32_e32 v154, v28, v154
	v_mul_f32_e32 v155, v28, v155
	ds_write_b128 v209, v[152:155] offset:2048
	v_mul_f32_e32 v156, v29, v156
	v_mul_f32_e32 v157, v29, v157
	v_mul_f32_e32 v158, v29, v158
	v_mul_f32_e32 v159, v29, v159
	ds_write_b128 v209, v[156:159] offset:3072
	v_mul_f32_e32 v160, v30, v160
	v_mul_f32_e32 v161, v30, v161
	v_mul_f32_e32 v162, v30, v162
	v_mul_f32_e32 v163, v30, v163
	ds_write_b128 v209, v[160:163] offset:4096
	v_mul_f32_e32 v164, v31, v164
	v_mul_f32_e32 v165, v31, v165
	v_mul_f32_e32 v166, v31, v166
	v_mul_f32_e32 v167, v31, v167
	ds_write_b128 v209, v[164:167] offset:5120
	v_mul_f32_e32 v168, v32, v168
	v_mul_f32_e32 v169, v32, v169
	v_mul_f32_e32 v170, v32, v170
	v_mul_f32_e32 v171, v32, v171
	ds_write_b128 v209, v[168:171] offset:6144
	v_mul_f32_e32 v172, v33, v172
	v_mul_f32_e32 v173, v33, v173
	v_mul_f32_e32 v174, v33, v174
	v_mul_f32_e32 v175, v33, v175
	ds_write_b128 v209, v[172:175] offset:7168
	s_waitcnt lgkmcnt(0)
	s_barrier
; #define GAS __attribute__((address_space(1)))
; #define LAS __attribute__((address_space(3)))
; #define LDS_WAIT() asm volatile("s_waitcnt lgkmcnt(0)" ::: "memory")
; __device__ __forceinline__ unsigned pk4_fp8(float a, float b, float c, float d) {
;     a = fminf(fmaxf(a, -448.f), 448.f); b = fminf(fmaxf(b, -448.f), 448.f); c = fminf(fmaxf(c, -448.f), 448.f); d = fminf(fmaxf(d, -448.f), 448.f);
;     int w = __builtin_amdgcn_cvt_pk_fp8_f32(a, b, 0, false); w = __builtin_amdgcn_cvt_pk_fp8_f32(c, d, w, true); return (unsigned)w; }
;     const int pr = item >> 1, kb = 2 * (pr / nblk) + (item & 1), nb = pr % nblk, k0 = 64 * kb, n0 = 32 * nb;
;     const int nr = n0 + (lane & 31); const int sc = MAP == 1 ? src_col_in(nr) : nr;
;     float v[32];
; #pragma unroll
;     for (int i = 0; i < 32; ++i) v[i] = sc >= 0 ? W[(size_t)(k0 + 2 * i + (lane >> 5)) * Nsrc + sc] : 0.f;
; #pragma unroll
;     for (int i = 0; i < 32; ++i) { const int k = k0 + 2 * i + (lane >> 5); float x = v[i] * wscale; if (KS) x *= (k < ksplit ? ksA[k] : ksB[k - ksplit]); scr[(2 * i + (lane >> 5)) * 33 + (lane & 31)] = x; }
;     LDS_WAIT(); asm volatile("" ::: "memory");
;     const int c = lane & 7;
; #pragma unroll
;     for (int j = 0; j < 4; ++j) { const int n = (lane >> 3) + 8 * j; const LAS float* s = scr + (8 * c) * 33 + n;
;         const unsigned long long o = (unsigned long long)pg8::pk4_fp8(s[0 * 33], s[1 * 33], s[2 * 33], s[3 * 33]) | ((unsigned long long)pg8::pk4_fp8(s[4 * 33], s[5 * 33], s[6 * 33], s[7 * 33]) << 32);
;         *(GAS unsigned long long*)(WT + (size_t)(n0 + n) * K + k0 + 8 * c) = o; }
;     LDS_WAIT(); asm volatile("" ::: "memory");
; }
	s_add_u32 s8, s30, 0xe000
	s_addc_u32 s9, s31, 0
	global_load_dwordx4 v[144:147], v74, s[8:9]
	s_add_u32 s8, s8, 0x20000
	s_addc_u32 s9, s9, 0
	global_load_dwordx4 v[148:151], v74, s[8:9]
	s_add_u32 s8, s8, 0x20000
	s_addc_u32 s9, s9, 0
	global_load_dwordx4 v[152:155], v74, s[8:9]
	s_add_u32 s8, s8, 0x20000
	s_addc_u32 s9, s9, 0
	global_load_dwordx4 v[156:159], v74, s[8:9]
	s_add_u32 s8, s8, 0x20000
	s_addc_u32 s9, s9, 0
	global_load_dwordx4 v[160:163], v74, s[8:9]
	s_add_u32 s8, s8, 0x20000
	s_addc_u32 s9, s9, 0
	global_load_dwordx4 v[164:167], v74, s[8:9]
	s_add_u32 s8, s8, 0x20000
	s_addc_u32 s9, s9, 0
	global_load_dwordx4 v[168:171], v74, s[8:9]
	s_add_u32 s8, s8, 0x20000
	s_addc_u32 s9, s9, 0
	global_load_dwordx4 v[172:175], v74, s[8:9]
	s_add_u32 s6, s32, 0x3000000
	s_addc_u32 s7, s33, 0
	ds_read_b32 v226, v211
	ds_read_b32 v227, v211 offset:512
	ds_read_b32 v228, v211 offset:1024
	ds_read_b32 v229, v211 offset:1536
	ds_read_b32 v230, v211 offset:2048
	ds_read_b32 v231, v211 offset:2560
	ds_read_b32 v232, v211 offset:3072
	ds_read_b32 v233, v211 offset:3584
	ds_read_b32 v234, v211 offset:4096
	ds_read_b32 v235, v211 offset:4608
	ds_read_b32 v236, v211 offset:5120
	ds_read_b32 v237, v211 offset:5632
	ds_read_b32 v238, v211 offset:6144
	ds_read_b32 v239, v211 offset:6656
	ds_read_b32 v240, v211 offset:7168
	ds_read_b32 v241, v211 offset:7680
	s_waitcnt lgkmcnt(0)
	v_max_f32_e32 v226, v226, v226
	v_max_f32_e32 v227, v227, v227
	v_max_f32_e32 v228, v228, v228
	v_max_f32_e32 v229, v229, v229
	v_max_f32_e32 v230, v230, v230
	v_max_f32_e32 v231, v231, v231
	v_max_f32_e32 v232, v232, v232
	v_max_f32_e32 v233, v233, v233
	v_max_f32_e32 v234, v234, v234
	v_max_f32_e32 v235, v235, v235
	v_max_f32_e32 v236, v236, v236
	v_max_f32_e32 v237, v237, v237
	v_max_f32_e32 v238, v238, v238
	v_max_f32_e32 v239, v239, v239
	v_max_f32_e32 v240, v240, v240
	v_max_f32_e32 v241, v241, v241
	v_med3_f32 v226, v226, s62, v95
	v_med3_f32 v227, v227, s62, v95
	v_med3_f32 v228, v228, s62, v95
	v_med3_f32 v229, v229, s62, v95
	v_med3_f32 v230, v230, s62, v95
	v_med3_f32 v231, v231, s62, v95
	v_med3_f32 v232, v232, s62, v95
	v_med3_f32 v233, v233, s62, v95
	v_med3_f32 v234, v234, s62, v95
	v_med3_f32 v235, v235, s62, v95
	v_med3_f32 v236, v236, s62, v95
	v_med3_f32 v237, v237, s62, v95
	v_med3_f32 v238, v238, s62, v95
	v_med3_f32 v239, v239, s62, v95
	v_med3_f32 v240, v240, s62, v95
	v_med3_f32 v241, v241, s62, v95
	v_mov_b32_e32 v242, 0
	v_mov_b32_e32 v243, 0
	v_mov_b32_e32 v244, 0
	v_mov_b32_e32 v245, 0
	v_cvt_pk_fp8_f32 v242, v226, v227
	v_cvt_pk_fp8_f32 v243, v230, v231
	v_cvt_pk_fp8_f32 v244, v234, v235
	v_cvt_pk_fp8_f32 v245, v238, v239
	v_cvt_pk_fp8_f32 v242, v228, v229 op_sel:[0,0,1]
	v_cvt_pk_fp8_f32 v243, v232, v233 op_sel:[0,0,1]
	v_cvt_pk_fp8_f32 v244, v236, v237 op_sel:[0,0,1]
	v_cvt_pk_fp8_f32 v245, v240, v241 op_sel:[0,0,1]
	s_nop 0
	global_store_dwordx4 v77, v[242:245], s[6:7]
	ds_read_b32 v226, v213
	ds_read_b32 v227, v213 offset:512
	ds_read_b32 v228, v213 offset:1024
	ds_read_b32 v229, v213 offset:1536
	ds_read_b32 v230, v213 offset:2048
	ds_read_b32 v231, v213 offset:2560
	ds_read_b32 v232, v213 offset:3072
	ds_read_b32 v233, v213 offset:3584
	ds_read_b32 v234, v213 offset:4096
	ds_read_b32 v235, v213 offset:4608
	ds_read_b32 v236, v213 offset:5120
	ds_read_b32 v237, v213 offset:5632
	ds_read_b32 v238, v213 offset:6144
	ds_read_b32 v239, v213 offset:6656
	ds_read_b32 v240, v213 offset:7168
	ds_read_b32 v241, v213 offset:7680
	s_waitcnt lgkmcnt(0)
	v_max_f32_e32 v226, v226, v226
	v_max_f32_e32 v227, v227, v227
	v_max_f32_e32 v228, v228, v228
	v_max_f32_e32 v229, v229, v229
	v_max_f32_e32 v230, v230, v230
	v_max_f32_e32 v231, v231, v231
	v_max_f32_e32 v232, v232, v232
	v_max_f32_e32 v233, v233, v233
	v_max_f32_e32 v234, v234, v234
	v_max_f32_e32 v235, v235, v235
	v_max_f32_e32 v236, v236, v236
	v_max_f32_e32 v237, v237, v237
	v_max_f32_e32 v238, v238, v238
	v_max_f32_e32 v239, v239, v239
	v_max_f32_e32 v240, v240, v240
	v_max_f32_e32 v241, v241, v241
	v_med3_f32 v226, v226, s62, v95
	v_med3_f32 v227, v227, s62, v95
	v_med3_f32 v228, v228, s62, v95
	v_med3_f32 v229, v229, s62, v95
	v_med3_f32 v230, v230, s62, v95
	v_med3_f32 v231, v231, s62, v95
	v_med3_f32 v232, v232, s62, v95
	v_med3_f32 v233, v233, s62, v95
	v_med3_f32 v234, v234, s62, v95
	v_med3_f32 v235, v235, s62, v95
	v_med3_f32 v236, v236, s62, v95
	v_med3_f32 v237, v237, s62, v95
	v_med3_f32 v238, v238, s62, v95
	v_med3_f32 v239, v239, s62, v95
	v_med3_f32 v240, v240, s62, v95
	v_med3_f32 v241, v241, s62, v95
	v_mov_b32_e32 v242, 0
	v_mov_b32_e32 v243, 0
	v_mov_b32_e32 v244, 0
	v_mov_b32_e32 v245, 0
	v_cvt_pk_fp8_f32 v242, v226, v227
	v_cvt_pk_fp8_f32 v243, v230, v231
	v_cvt_pk_fp8_f32 v244, v234, v235
	v_cvt_pk_fp8_f32 v245, v238, v239
	v_cvt_pk_fp8_f32 v242, v228, v229 op_sel:[0,0,1]
	v_cvt_pk_fp8_f32 v243, v232, v233 op_sel:[0,0,1]
	v_cvt_pk_fp8_f32 v244, v236, v237 op_sel:[0,0,1]
	v_cvt_pk_fp8_f32 v245, v240, v241 op_sel:[0,0,1]
	s_nop 0
	global_store_dwordx4 v78, v[242:245], s[6:7]
	s_waitcnt vmcnt(12)
	v_mul_f32_e32 v176, v26, v176
	v_mul_f32_e32 v177, v26, v177
	v_mul_f32_e32 v178, v26, v178
	v_mul_f32_e32 v179, v26, v179
	ds_write_b128 v210, v[176:179]
	v_mul_f32_e32 v180, v27, v180
	v_mul_f32_e32 v181, v27, v181
	v_mul_f32_e32 v182, v27, v182
	v_mul_f32_e32 v183, v27, v183
	ds_write_b128 v210, v[180:183] offset:1024
	v_mul_f32_e32 v184, v28, v184
	v_mul_f32_e32 v185, v28, v185
	v_mul_f32_e32 v186, v28, v186
	v_mul_f32_e32 v187, v28, v187
	ds_write_b128 v210, v[184:187] offset:2048
	v_mul_f32_e32 v188, v29, v188
	v_mul_f32_e32 v189, v29, v189
	v_mul_f32_e32 v190, v29, v190
	v_mul_f32_e32 v191, v29, v191
	ds_write_b128 v210, v[188:191] offset:3072
	v_mul_f32_e32 v192, v30, v192
	v_mul_f32_e32 v193, v30, v193
	v_mul_f32_e32 v194, v30, v194
	v_mul_f32_e32 v195, v30, v195
	ds_write_b128 v210, v[192:195] offset:4096
	v_mul_f32_e32 v196, v31, v196
	v_mul_f32_e32 v197, v31, v197
	v_mul_f32_e32 v198, v31, v198
	v_mul_f32_e32 v199, v31, v199
	ds_write_b128 v210, v[196:199] offset:5120
	v_mul_f32_e32 v200, v32, v200
	v_mul_f32_e32 v201, v32, v201
	v_mul_f32_e32 v202, v32, v202
	v_mul_f32_e32 v203, v32, v203
	ds_write_b128 v210, v[200:203] offset:6144
	v_mul_f32_e32 v204, v33, v204
	v_mul_f32_e32 v205, v33, v205
	v_mul_f32_e32 v206, v33, v206
	v_mul_f32_e32 v207, v33, v207
	ds_write_b128 v210, v[204:207] offset:7168
	s_waitcnt lgkmcnt(0)
	s_barrier
; #define GAS __attribute__((address_space(1)))
; #define LAS __attribute__((address_space(3)))
; #define LDS_WAIT() asm volatile("s_waitcnt lgkmcnt(0)" ::: "memory")
; __device__ __forceinline__ unsigned pk4_fp8(float a, float b, float c, float d) {
;     a = fminf(fmaxf(a, -448.f), 448.f); b = fminf(fmaxf(b, -448.f), 448.f); c = fminf(fmaxf(c, -448.f), 448.f); d = fminf(fmaxf(d, -448.f), 448.f);
;     int w = __builtin_amdgcn_cvt_pk_fp8_f32(a, b, 0, false); w = __builtin_amdgcn_cvt_pk_fp8_f32(c, d, w, true); return (unsigned)w; }
;     const int pr = item >> 1, kb = 2 * (pr / nblk) + (item & 1), nb = pr % nblk, k0 = 64 * kb, n0 = 32 * nb;
;     const int nr = n0 + (lane & 31); const int sc = MAP == 1 ? src_col_in(nr) : nr;
;     float v[32];
; #pragma unroll
;     for (int i = 0; i < 32; ++i) v[i] = sc >= 0 ? W[(size_t)(k0 + 2 * i + (lane >> 5)) * Nsrc + sc] : 0.f;
; #pragma unroll
;     for (int i = 0; i < 32; ++i) { const int k = k0 + 2 * i + (lane >> 5); float x = v[i] * wscale; if (KS) x *= (k < ksplit ? ksA[k] : ksB[k - ksplit]); scr[(2 * i + (lane >> 5)) * 33 + (lane & 31)] = x; }
;     LDS_WAIT(); asm volatile("" ::: "memory");
;     const int c = lane & 7;
; #pragma unroll
;     for (int j = 0; j < 4; ++j) { const int n = (lane >> 3) + 8 * j; const LAS float* s = scr + (8 * c) * 33 + n;
;         const unsigned long long o = (unsigned long long)pg8::pk4_fp8(s[0 * 33], s[1 * 33], s[2 * 33], s[3 * 33]) | ((unsigned long long)pg8::pk4_fp8(s[4 * 33], s[5 * 33], s[6 * 33], s[7 * 33]) << 32);
;         *(GAS unsigned long long*)(WT + (size_t)(n0 + n) * K + k0 + 8 * c) = o; }
;     LDS_WAIT(); asm volatile("" ::: "memory");
; }
	s_add_u32 s8, s30, 0xf000
	s_addc_u32 s9, s31, 0
	global_load_dwordx4 v[176:179], v74, s[8:9]
	s_add_u32 s8, s8, 0x20000
	s_addc_u32 s9, s9, 0
	global_load_dwordx4 v[180:183], v74, s[8:9]
	s_add_u32 s8, s8, 0x20000
	s_addc_u32 s9, s9, 0
	global_load_dwordx4 v[184:187], v74, s[8:9]
	s_add_u32 s8, s8, 0x20000
	s_addc_u32 s9, s9, 0
	global_load_dwordx4 v[188:191], v74, s[8:9]
	s_add_u32 s8, s8, 0x20000
	s_addc_u32 s9, s9, 0
	global_load_dwordx4 v[192:195], v74, s[8:9]
	s_add_u32 s8, s8, 0x20000
	s_addc_u32 s9, s9, 0
	global_load_dwordx4 v[196:199], v74, s[8:9]
	s_add_u32 s8, s8, 0x20000
	s_addc_u32 s9, s9, 0
	global_load_dwordx4 v[200:203], v74, s[8:9]
	s_add_u32 s8, s8, 0x20000
	s_addc_u32 s9, s9, 0
	global_load_dwordx4 v[204:207], v74, s[8:9]
	s_add_u32 s6, s32, 0x3400000
	s_addc_u32 s7, s33, 0
	ds_read_b32 v226, v212
	ds_read_b32 v227, v212 offset:512
	ds_read_b32 v228, v212 offset:1024
	ds_read_b32 v229, v212 offset:1536
	ds_read_b32 v230, v212 offset:2048
	ds_read_b32 v231, v212 offset:2560
	ds_read_b32 v232, v212 offset:3072
	ds_read_b32 v233, v212 offset:3584
	ds_read_b32 v234, v212 offset:4096
	ds_read_b32 v235, v212 offset:4608
	ds_read_b32 v236, v212 offset:5120
	ds_read_b32 v237, v212 offset:5632
	ds_read_b32 v238, v212 offset:6144
	ds_read_b32 v239, v212 offset:6656
	ds_read_b32 v240, v212 offset:7168
	ds_read_b32 v241, v212 offset:7680
	s_waitcnt lgkmcnt(0)
	v_max_f32_e32 v226, v226, v226
	v_max_f32_e32 v227, v227, v227
	v_max_f32_e32 v228, v228, v228
	v_max_f32_e32 v229, v229, v229
	v_max_f32_e32 v230, v230, v230
	v_max_f32_e32 v231, v231, v231
	v_max_f32_e32 v232, v232, v232
	v_max_f32_e32 v233, v233, v233
	v_max_f32_e32 v234, v234, v234
	v_max_f32_e32 v235, v235, v235
	v_max_f32_e32 v236, v236, v236
	v_max_f32_e32 v237, v237, v237
	v_max_f32_e32 v238, v238, v238
	v_max_f32_e32 v239, v239, v239
	v_max_f32_e32 v240, v240, v240
	v_max_f32_e32 v241, v241, v241
	v_med3_f32 v226, v226, s62, v95
	v_med3_f32 v227, v227, s62, v95
	v_med3_f32 v228, v228, s62, v95
	v_med3_f32 v229, v229, s62, v95
	v_med3_f32 v230, v230, s62, v95
	v_med3_f32 v231, v231, s62, v95
	v_med3_f32 v232, v232, s62, v95
	v_med3_f32 v233, v233, s62, v95
	v_med3_f32 v234, v234, s62, v95
	v_med3_f32 v235, v235, s62, v95
	v_med3_f32 v236, v236, s62, v95
	v_med3_f32 v237, v237, s62, v95
	v_med3_f32 v238, v238, s62, v95
	v_med3_f32 v239, v239, s62, v95
	v_med3_f32 v240, v240, s62, v95
	v_med3_f32 v241, v241, s62, v95
	v_mov_b32_e32 v242, 0
	v_mov_b32_e32 v243, 0
	v_mov_b32_e32 v244, 0
	v_mov_b32_e32 v245, 0
	v_cvt_pk_fp8_f32 v242, v226, v227
	v_cvt_pk_fp8_f32 v243, v230, v231
	v_cvt_pk_fp8_f32 v244, v234, v235
	v_cvt_pk_fp8_f32 v245, v238, v239
	v_cvt_pk_fp8_f32 v242, v228, v229 op_sel:[0,0,1]
	v_cvt_pk_fp8_f32 v243, v232, v233 op_sel:[0,0,1]
	v_cvt_pk_fp8_f32 v244, v236, v237 op_sel:[0,0,1]
	v_cvt_pk_fp8_f32 v245, v240, v241 op_sel:[0,0,1]
	s_nop 0
	global_store_dwordx4 v77, v[242:245], s[6:7]
	ds_read_b32 v226, v214
	ds_read_b32 v227, v214 offset:512
	ds_read_b32 v228, v214 offset:1024
	ds_read_b32 v229, v214 offset:1536
	ds_read_b32 v230, v214 offset:2048
	ds_read_b32 v231, v214 offset:2560
	ds_read_b32 v232, v214 offset:3072
	ds_read_b32 v233, v214 offset:3584
	ds_read_b32 v234, v214 offset:4096
	ds_read_b32 v235, v214 offset:4608
	ds_read_b32 v236, v214 offset:5120
	ds_read_b32 v237, v214 offset:5632
	ds_read_b32 v238, v214 offset:6144
	ds_read_b32 v239, v214 offset:6656
	ds_read_b32 v240, v214 offset:7168
	ds_read_b32 v241, v214 offset:7680
	s_waitcnt lgkmcnt(0)
	v_max_f32_e32 v226, v226, v226
	v_max_f32_e32 v227, v227, v227
	v_max_f32_e32 v228, v228, v228
	v_max_f32_e32 v229, v229, v229
	v_max_f32_e32 v230, v230, v230
	v_max_f32_e32 v231, v231, v231
	v_max_f32_e32 v232, v232, v232
	v_max_f32_e32 v233, v233, v233
	v_max_f32_e32 v234, v234, v234
	v_max_f32_e32 v235, v235, v235
	v_max_f32_e32 v236, v236, v236
	v_max_f32_e32 v237, v237, v237
	v_max_f32_e32 v238, v238, v238
	v_max_f32_e32 v239, v239, v239
	v_max_f32_e32 v240, v240, v240
	v_max_f32_e32 v241, v241, v241
	v_med3_f32 v226, v226, s62, v95
	v_med3_f32 v227, v227, s62, v95
	v_med3_f32 v228, v228, s62, v95
	v_med3_f32 v229, v229, s62, v95
	v_med3_f32 v230, v230, s62, v95
	v_med3_f32 v231, v231, s62, v95
	v_med3_f32 v232, v232, s62, v95
	v_med3_f32 v233, v233, s62, v95
	v_med3_f32 v234, v234, s62, v95
	v_med3_f32 v235, v235, s62, v95
	v_med3_f32 v236, v236, s62, v95
	v_med3_f32 v237, v237, s62, v95
	v_med3_f32 v238, v238, s62, v95
	v_med3_f32 v239, v239, s62, v95
	v_med3_f32 v240, v240, s62, v95
	v_med3_f32 v241, v241, s62, v95
	v_mov_b32_e32 v242, 0
	v_mov_b32_e32 v243, 0
	v_mov_b32_e32 v244, 0
	v_mov_b32_e32 v245, 0
	v_cvt_pk_fp8_f32 v242, v226, v227
	v_cvt_pk_fp8_f32 v243, v230, v231
	v_cvt_pk_fp8_f32 v244, v234, v235
	v_cvt_pk_fp8_f32 v245, v238, v239
	v_cvt_pk_fp8_f32 v242, v228, v229 op_sel:[0,0,1]
	v_cvt_pk_fp8_f32 v243, v232, v233 op_sel:[0,0,1]
	v_cvt_pk_fp8_f32 v244, v236, v237 op_sel:[0,0,1]
	v_cvt_pk_fp8_f32 v245, v240, v241 op_sel:[0,0,1]
	s_nop 0
	global_store_dwordx4 v78, v[242:245], s[6:7]
	s_waitcnt vmcnt(12)
	v_mul_f32_e32 v144, v26, v144
	v_mul_f32_e32 v145, v26, v145
	v_mul_f32_e32 v146, v26, v146
	v_mul_f32_e32 v147, v26, v147
	ds_write_b128 v209, v[144:147]
	v_mul_f32_e32 v148, v27, v148
	v_mul_f32_e32 v149, v27, v149
	v_mul_f32_e32 v150, v27, v150
	v_mul_f32_e32 v151, v27, v151
	ds_write_b128 v209, v[148:151] offset:1024
	v_mul_f32_e32 v152, v28, v152
	v_mul_f32_e32 v153, v28, v153
	v_mul_f32_e32 v154, v28, v154
	v_mul_f32_e32 v155, v28, v155
	ds_write_b128 v209, v[152:155] offset:2048
	v_mul_f32_e32 v156, v29, v156
	v_mul_f32_e32 v157, v29, v157
	v_mul_f32_e32 v158, v29, v158
	v_mul_f32_e32 v159, v29, v159
	ds_write_b128 v209, v[156:159] offset:3072
	v_mul_f32_e32 v160, v30, v160
	v_mul_f32_e32 v161, v30, v161
	v_mul_f32_e32 v162, v30, v162
	v_mul_f32_e32 v163, v30, v163
	ds_write_b128 v209, v[160:163] offset:4096
	v_mul_f32_e32 v164, v31, v164
	v_mul_f32_e32 v165, v31, v165
	v_mul_f32_e32 v166, v31, v166
	v_mul_f32_e32 v167, v31, v167
	ds_write_b128 v209, v[164:167] offset:5120
	v_mul_f32_e32 v168, v32, v168
	v_mul_f32_e32 v169, v32, v169
	v_mul_f32_e32 v170, v32, v170
	v_mul_f32_e32 v171, v32, v171
	ds_write_b128 v209, v[168:171] offset:6144
	v_mul_f32_e32 v172, v33, v172
	v_mul_f32_e32 v173, v33, v173
	v_mul_f32_e32 v174, v33, v174
	v_mul_f32_e32 v175, v33, v175
	ds_write_b128 v209, v[172:175] offset:7168
	s_waitcnt lgkmcnt(0)
	s_barrier
; #define GAS __attribute__((address_space(1)))
; #define LAS __attribute__((address_space(3)))
; #define LDS_WAIT() asm volatile("s_waitcnt lgkmcnt(0)" ::: "memory")
; __device__ __forceinline__ unsigned pk4_fp8(float a, float b, float c, float d) {
;     a = fminf(fmaxf(a, -448.f), 448.f); b = fminf(fmaxf(b, -448.f), 448.f); c = fminf(fmaxf(c, -448.f), 448.f); d = fminf(fmaxf(d, -448.f), 448.f);
;     int w = __builtin_amdgcn_cvt_pk_fp8_f32(a, b, 0, false); w = __builtin_amdgcn_cvt_pk_fp8_f32(c, d, w, true); return (unsigned)w; }
;     const int pr = item >> 1, kb = 2 * (pr / nblk) + (item & 1), nb = pr % nblk, k0 = 64 * kb, n0 = 32 * nb;
;     const int nr = n0 + (lane & 31); const int sc = MAP == 1 ? src_col_in(nr) : nr;
;     float v[32];
; #pragma unroll
;     for (int i = 0; i < 32; ++i) v[i] = sc >= 0 ? W[(size_t)(k0 + 2 * i + (lane >> 5)) * Nsrc + sc] : 0.f;
; #pragma unroll
;     for (int i = 0; i < 32; ++i) { const int k = k0 + 2 * i + (lane >> 5); float x = v[i] * wscale; if (KS) x *= (k < ksplit ? ksA[k] : ksB[k - ksplit]); scr[(2 * i + (lane >> 5)) * 33 + (lane & 31)] = x; }
;     LDS_WAIT(); asm volatile("" ::: "memory");
;     const int c = lane & 7;
; #pragma unroll
;     for (int j = 0; j < 4; ++j) { const int n = (lane >> 3) + 8 * j; const LAS float* s = scr + (8 * c) * 33 + n;
;         const unsigned long long o = (unsigned long long)pg8::pk4_fp8(s[0 * 33], s[1 * 33], s[2 * 33], s[3 * 33]) | ((unsigned long long)pg8::pk4_fp8(s[4 * 33], s[5 * 33], s[6 * 33], s[7 * 33]) << 32);
;         *(GAS unsigned long long*)(WT + (size_t)(n0 + n) * K + k0 + 8 * c) = o; }
;     LDS_WAIT(); asm volatile("" ::: "memory");
; }
	s_mov_b64 s[8:9], s[34:35]
	global_load_dwordx4 v[144:147], v74, s[8:9]
	s_add_u32 s8, s8, 0x20000
	s_addc_u32 s9, s9, 0
	global_load_dwordx4 v[148:151], v74, s[8:9]
	s_add_u32 s8, s8, 0x20000
	s_addc_u32 s9, s9, 0
	global_load_dwordx4 v[152:155], v74, s[8:9]
	s_add_u32 s8, s8, 0x20000
	s_addc_u32 s9, s9, 0
	global_load_dwordx4 v[156:159], v74, s[8:9]
	s_add_u32 s8, s8, 0x20000
	s_addc_u32 s9, s9, 0
	global_load_dwordx4 v[160:163], v74, s[8:9]
	s_add_u32 s8, s8, 0x20000
	s_addc_u32 s9, s9, 0
	global_load_dwordx4 v[164:167], v74, s[8:9]
	s_add_u32 s8, s8, 0x20000
	s_addc_u32 s9, s9, 0
	global_load_dwordx4 v[168:171], v74, s[8:9]
	s_add_u32 s8, s8, 0x20000
	s_addc_u32 s9, s9, 0
	global_load_dwordx4 v[172:175], v74, s[8:9]
	s_add_u32 s6, s32, 0x3800000
	s_addc_u32 s7, s33, 0
	ds_read_b32 v226, v211
	ds_read_b32 v227, v211 offset:512
	ds_read_b32 v228, v211 offset:1024
	ds_read_b32 v229, v211 offset:1536
	ds_read_b32 v230, v211 offset:2048
	ds_read_b32 v231, v211 offset:2560
	ds_read_b32 v232, v211 offset:3072
	ds_read_b32 v233, v211 offset:3584
	ds_read_b32 v234, v211 offset:4096
	ds_read_b32 v235, v211 offset:4608
	ds_read_b32 v236, v211 offset:5120
	ds_read_b32 v237, v211 offset:5632
	ds_read_b32 v238, v211 offset:6144
	ds_read_b32 v239, v211 offset:6656
	ds_read_b32 v240, v211 offset:7168
	ds_read_b32 v241, v211 offset:7680
	s_waitcnt lgkmcnt(0)
	v_max_f32_e32 v226, v226, v226
	v_max_f32_e32 v227, v227, v227
	v_max_f32_e32 v228, v228, v228
	v_max_f32_e32 v229, v229, v229
	v_max_f32_e32 v230, v230, v230
	v_max_f32_e32 v231, v231, v231
	v_max_f32_e32 v232, v232, v232
	v_max_f32_e32 v233, v233, v233
	v_max_f32_e32 v234, v234, v234
	v_max_f32_e32 v235, v235, v235
	v_max_f32_e32 v236, v236, v236
	v_max_f32_e32 v237, v237, v237
	v_max_f32_e32 v238, v238, v238
	v_max_f32_e32 v239, v239, v239
	v_max_f32_e32 v240, v240, v240
	v_max_f32_e32 v241, v241, v241
	v_med3_f32 v226, v226, s62, v95
	v_med3_f32 v227, v227, s62, v95
	v_med3_f32 v228, v228, s62, v95
	v_med3_f32 v229, v229, s62, v95
	v_med3_f32 v230, v230, s62, v95
	v_med3_f32 v231, v231, s62, v95
	v_med3_f32 v232, v232, s62, v95
	v_med3_f32 v233, v233, s62, v95
	v_med3_f32 v234, v234, s62, v95
	v_med3_f32 v235, v235, s62, v95
	v_med3_f32 v236, v236, s62, v95
	v_med3_f32 v237, v237, s62, v95
	v_med3_f32 v238, v238, s62, v95
	v_med3_f32 v239, v239, s62, v95
	v_med3_f32 v240, v240, s62, v95
	v_med3_f32 v241, v241, s62, v95
	v_mov_b32_e32 v242, 0
	v_mov_b32_e32 v243, 0
	v_mov_b32_e32 v244, 0
	v_mov_b32_e32 v245, 0
	v_cvt_pk_fp8_f32 v242, v226, v227
	v_cvt_pk_fp8_f32 v243, v230, v231
	v_cvt_pk_fp8_f32 v244, v234, v235
	v_cvt_pk_fp8_f32 v245, v238, v239
	v_cvt_pk_fp8_f32 v242, v228, v229 op_sel:[0,0,1]
	v_cvt_pk_fp8_f32 v243, v232, v233 op_sel:[0,0,1]
	v_cvt_pk_fp8_f32 v244, v236, v237 op_sel:[0,0,1]
	v_cvt_pk_fp8_f32 v245, v240, v241 op_sel:[0,0,1]
	s_nop 0
	global_store_dwordx4 v77, v[242:245], s[6:7]
	ds_read_b32 v226, v213
	ds_read_b32 v227, v213 offset:512
	ds_read_b32 v228, v213 offset:1024
	ds_read_b32 v229, v213 offset:1536
	ds_read_b32 v230, v213 offset:2048
	ds_read_b32 v231, v213 offset:2560
	ds_read_b32 v232, v213 offset:3072
	ds_read_b32 v233, v213 offset:3584
	ds_read_b32 v234, v213 offset:4096
	ds_read_b32 v235, v213 offset:4608
	ds_read_b32 v236, v213 offset:5120
	ds_read_b32 v237, v213 offset:5632
	ds_read_b32 v238, v213 offset:6144
	ds_read_b32 v239, v213 offset:6656
	ds_read_b32 v240, v213 offset:7168
	ds_read_b32 v241, v213 offset:7680
	s_waitcnt lgkmcnt(0)
	v_max_f32_e32 v226, v226, v226
	v_max_f32_e32 v227, v227, v227
	v_max_f32_e32 v228, v228, v228
	v_max_f32_e32 v229, v229, v229
	v_max_f32_e32 v230, v230, v230
	v_max_f32_e32 v231, v231, v231
	v_max_f32_e32 v232, v232, v232
	v_max_f32_e32 v233, v233, v233
	v_max_f32_e32 v234, v234, v234
	v_max_f32_e32 v235, v235, v235
	v_max_f32_e32 v236, v236, v236
	v_max_f32_e32 v237, v237, v237
	v_max_f32_e32 v238, v238, v238
	v_max_f32_e32 v239, v239, v239
	v_max_f32_e32 v240, v240, v240
	v_max_f32_e32 v241, v241, v241
	v_med3_f32 v226, v226, s62, v95
	v_med3_f32 v227, v227, s62, v95
	v_med3_f32 v228, v228, s62, v95
	v_med3_f32 v229, v229, s62, v95
	v_med3_f32 v230, v230, s62, v95
	v_med3_f32 v231, v231, s62, v95
	v_med3_f32 v232, v232, s62, v95
	v_med3_f32 v233, v233, s62, v95
	v_med3_f32 v234, v234, s62, v95
	v_med3_f32 v235, v235, s62, v95
	v_med3_f32 v236, v236, s62, v95
	v_med3_f32 v237, v237, s62, v95
	v_med3_f32 v238, v238, s62, v95
	v_med3_f32 v239, v239, s62, v95
	v_med3_f32 v240, v240, s62, v95
	v_med3_f32 v241, v241, s62, v95
	v_mov_b32_e32 v242, 0
	v_mov_b32_e32 v243, 0
	v_mov_b32_e32 v244, 0
	v_mov_b32_e32 v245, 0
	v_cvt_pk_fp8_f32 v242, v226, v227
	v_cvt_pk_fp8_f32 v243, v230, v231
	v_cvt_pk_fp8_f32 v244, v234, v235
	v_cvt_pk_fp8_f32 v245, v238, v239
	v_cvt_pk_fp8_f32 v242, v228, v229 op_sel:[0,0,1]
	v_cvt_pk_fp8_f32 v243, v232, v233 op_sel:[0,0,1]
	v_cvt_pk_fp8_f32 v244, v236, v237 op_sel:[0,0,1]
	v_cvt_pk_fp8_f32 v245, v240, v241 op_sel:[0,0,1]
	s_nop 0
	global_store_dwordx4 v78, v[242:245], s[6:7]
	s_waitcnt vmcnt(12)
	v_mul_f32_e32 v176, v26, v176
	v_mul_f32_e32 v177, v26, v177
	v_mul_f32_e32 v178, v26, v178
	v_mul_f32_e32 v179, v26, v179
	ds_write_b128 v210, v[176:179]
	v_mul_f32_e32 v180, v27, v180
	v_mul_f32_e32 v181, v27, v181
	v_mul_f32_e32 v182, v27, v182
	v_mul_f32_e32 v183, v27, v183
	ds_write_b128 v210, v[180:183] offset:1024
	v_mul_f32_e32 v184, v28, v184
	v_mul_f32_e32 v185, v28, v185
	v_mul_f32_e32 v186, v28, v186
	v_mul_f32_e32 v187, v28, v187
	ds_write_b128 v210, v[184:187] offset:2048
	v_mul_f32_e32 v188, v29, v188
	v_mul_f32_e32 v189, v29, v189
	v_mul_f32_e32 v190, v29, v190
	v_mul_f32_e32 v191, v29, v191
	ds_write_b128 v210, v[188:191] offset:3072
	v_mul_f32_e32 v192, v30, v192
	v_mul_f32_e32 v193, v30, v193
	v_mul_f32_e32 v194, v30, v194
	v_mul_f32_e32 v195, v30, v195
	ds_write_b128 v210, v[192:195] offset:4096
	v_mul_f32_e32 v196, v31, v196
	v_mul_f32_e32 v197, v31, v197
	v_mul_f32_e32 v198, v31, v198
	v_mul_f32_e32 v199, v31, v199
	ds_write_b128 v210, v[196:199] offset:5120
	v_mul_f32_e32 v200, v32, v200
	v_mul_f32_e32 v201, v32, v201
	v_mul_f32_e32 v202, v32, v202
	v_mul_f32_e32 v203, v32, v203
	ds_write_b128 v210, v[200:203] offset:6144
	v_mul_f32_e32 v204, v33, v204
	v_mul_f32_e32 v205, v33, v205
	v_mul_f32_e32 v206, v33, v206
	v_mul_f32_e32 v207, v33, v207
	ds_write_b128 v210, v[204:207] offset:7168
	s_waitcnt lgkmcnt(0)
	s_barrier
; #define GAS __attribute__((address_space(1)))
; #define LAS __attribute__((address_space(3)))
; #define LDS_WAIT() asm volatile("s_waitcnt lgkmcnt(0)" ::: "memory")
; __device__ __forceinline__ unsigned pk4_fp8(float a, float b, float c, float d) {
;     a = fminf(fmaxf(a, -448.f), 448.f); b = fminf(fmaxf(b, -448.f), 448.f); c = fminf(fmaxf(c, -448.f), 448.f); d = fminf(fmaxf(d, -448.f), 448.f);
;     int w = __builtin_amdgcn_cvt_pk_fp8_f32(a, b, 0, false); w = __builtin_amdgcn_cvt_pk_fp8_f32(c, d, w, true); return (unsigned)w; }
;     const int pr = item >> 1, kb = 2 * (pr / nblk) + (item & 1), nb = pr % nblk, k0 = 64 * kb, n0 = 32 * nb;
;     const int nr = n0 + (lane & 31); const int sc = MAP == 1 ? src_col_in(nr) : nr;
;     float v[32];
; #pragma unroll
;     for (int i = 0; i < 32; ++i) v[i] = sc >= 0 ? W[(size_t)(k0 + 2 * i + (lane >> 5)) * Nsrc + sc] : 0.f;
; #pragma unroll
;     for (int i = 0; i < 32; ++i) { const int k = k0 + 2 * i + (lane >> 5); float x = v[i] * wscale; if (KS) x *= (k < ksplit ? ksA[k] : ksB[k - ksplit]); scr[(2 * i + (lane >> 5)) * 33 + (lane & 31)] = x; }
;     LDS_WAIT(); asm volatile("" ::: "memory");
;     const int c = lane & 7;
; #pragma unroll
;     for (int j = 0; j < 4; ++j) { const int n = (lane >> 3) + 8 * j; const LAS float* s = scr + (8 * c) * 33 + n;
;         const unsigned long long o = (unsigned long long)pg8::pk4_fp8(s[0 * 33], s[1 * 33], s[2 * 33], s[3 * 33]) | ((unsigned long long)pg8::pk4_fp8(s[4 * 33], s[5 * 33], s[6 * 33], s[7 * 33]) << 32);
;         *(GAS unsigned long long*)(WT + (size_t)(n0 + n) * K + k0 + 8 * c) = o; }
;     LDS_WAIT(); asm volatile("" ::: "memory");
; }
	s_add_u32 s8, s34, 0x1000
	s_addc_u32 s9, s35, 0
	global_load_dwordx4 v[176:179], v74, s[8:9]
	s_add_u32 s8, s8, 0x20000
	s_addc_u32 s9, s9, 0
	global_load_dwordx4 v[180:183], v74, s[8:9]
	s_add_u32 s8, s8, 0x20000
	s_addc_u32 s9, s9, 0
	global_load_dwordx4 v[184:187], v74, s[8:9]
	s_add_u32 s8, s8, 0x20000
	s_addc_u32 s9, s9, 0
	global_load_dwordx4 v[188:191], v74, s[8:9]
	s_add_u32 s8, s8, 0x20000
	s_addc_u32 s9, s9, 0
	global_load_dwordx4 v[192:195], v74, s[8:9]
	s_add_u32 s8, s8, 0x20000
	s_addc_u32 s9, s9, 0
	global_load_dwordx4 v[196:199], v74, s[8:9]
	s_add_u32 s8, s8, 0x20000
	s_addc_u32 s9, s9, 0
	global_load_dwordx4 v[200:203], v74, s[8:9]
	s_add_u32 s8, s8, 0x20000
	s_addc_u32 s9, s9, 0
	global_load_dwordx4 v[204:207], v74, s[8:9]
	s_add_u32 s6, s32, 0x3c00000
	s_addc_u32 s7, s33, 0
	ds_read_b32 v226, v212
	ds_read_b32 v227, v212 offset:512
	ds_read_b32 v228, v212 offset:1024
	ds_read_b32 v229, v212 offset:1536
	ds_read_b32 v230, v212 offset:2048
	ds_read_b32 v231, v212 offset:2560
	ds_read_b32 v232, v212 offset:3072
	ds_read_b32 v233, v212 offset:3584
	ds_read_b32 v234, v212 offset:4096
	ds_read_b32 v235, v212 offset:4608
	ds_read_b32 v236, v212 offset:5120
	ds_read_b32 v237, v212 offset:5632
	ds_read_b32 v238, v212 offset:6144
	ds_read_b32 v239, v212 offset:6656
	ds_read_b32 v240, v212 offset:7168
	ds_read_b32 v241, v212 offset:7680
	s_waitcnt lgkmcnt(0)
	v_max_f32_e32 v226, v226, v226
	v_max_f32_e32 v227, v227, v227
	v_max_f32_e32 v228, v228, v228
	v_max_f32_e32 v229, v229, v229
	v_max_f32_e32 v230, v230, v230
	v_max_f32_e32 v231, v231, v231
	v_max_f32_e32 v232, v232, v232
	v_max_f32_e32 v233, v233, v233
	v_max_f32_e32 v234, v234, v234
	v_max_f32_e32 v235, v235, v235
	v_max_f32_e32 v236, v236, v236
	v_max_f32_e32 v237, v237, v237
	v_max_f32_e32 v238, v238, v238
	v_max_f32_e32 v239, v239, v239
	v_max_f32_e32 v240, v240, v240
	v_max_f32_e32 v241, v241, v241
	v_med3_f32 v226, v226, s62, v95
	v_med3_f32 v227, v227, s62, v95
	v_med3_f32 v228, v228, s62, v95
	v_med3_f32 v229, v229, s62, v95
	v_med3_f32 v230, v230, s62, v95
	v_med3_f32 v231, v231, s62, v95
	v_med3_f32 v232, v232, s62, v95
	v_med3_f32 v233, v233, s62, v95
	v_med3_f32 v234, v234, s62, v95
	v_med3_f32 v235, v235, s62, v95
	v_med3_f32 v236, v236, s62, v95
	v_med3_f32 v237, v237, s62, v95
	v_med3_f32 v238, v238, s62, v95
	v_med3_f32 v239, v239, s62, v95
	v_med3_f32 v240, v240, s62, v95
	v_med3_f32 v241, v241, s62, v95
	v_mov_b32_e32 v242, 0
	v_mov_b32_e32 v243, 0
	v_mov_b32_e32 v244, 0
	v_mov_b32_e32 v245, 0
	v_cvt_pk_fp8_f32 v242, v226, v227
	v_cvt_pk_fp8_f32 v243, v230, v231
	v_cvt_pk_fp8_f32 v244, v234, v235
	v_cvt_pk_fp8_f32 v245, v238, v239
	v_cvt_pk_fp8_f32 v242, v228, v229 op_sel:[0,0,1]
	v_cvt_pk_fp8_f32 v243, v232, v233 op_sel:[0,0,1]
	v_cvt_pk_fp8_f32 v244, v236, v237 op_sel:[0,0,1]
	v_cvt_pk_fp8_f32 v245, v240, v241 op_sel:[0,0,1]
	s_nop 0
	global_store_dwordx4 v77, v[242:245], s[6:7]
	ds_read_b32 v226, v214
	ds_read_b32 v227, v214 offset:512
	ds_read_b32 v228, v214 offset:1024
	ds_read_b32 v229, v214 offset:1536
	ds_read_b32 v230, v214 offset:2048
	ds_read_b32 v231, v214 offset:2560
	ds_read_b32 v232, v214 offset:3072
	ds_read_b32 v233, v214 offset:3584
	ds_read_b32 v234, v214 offset:4096
	ds_read_b32 v235, v214 offset:4608
	ds_read_b32 v236, v214 offset:5120
	ds_read_b32 v237, v214 offset:5632
	ds_read_b32 v238, v214 offset:6144
	ds_read_b32 v239, v214 offset:6656
	ds_read_b32 v240, v214 offset:7168
	ds_read_b32 v241, v214 offset:7680
	s_waitcnt lgkmcnt(0)
	v_max_f32_e32 v226, v226, v226
	v_max_f32_e32 v227, v227, v227
	v_max_f32_e32 v228, v228, v228
	v_max_f32_e32 v229, v229, v229
	v_max_f32_e32 v230, v230, v230
	v_max_f32_e32 v231, v231, v231
	v_max_f32_e32 v232, v232, v232
	v_max_f32_e32 v233, v233, v233
	v_max_f32_e32 v234, v234, v234
	v_max_f32_e32 v235, v235, v235
	v_max_f32_e32 v236, v236, v236
	v_max_f32_e32 v237, v237, v237
	v_max_f32_e32 v238, v238, v238
	v_max_f32_e32 v239, v239, v239
	v_max_f32_e32 v240, v240, v240
	v_max_f32_e32 v241, v241, v241
	v_med3_f32 v226, v226, s62, v95
	v_med3_f32 v227, v227, s62, v95
	v_med3_f32 v228, v228, s62, v95
	v_med3_f32 v229, v229, s62, v95
	v_med3_f32 v230, v230, s62, v95
	v_med3_f32 v231, v231, s62, v95
	v_med3_f32 v232, v232, s62, v95
	v_med3_f32 v233, v233, s62, v95
	v_med3_f32 v234, v234, s62, v95
	v_med3_f32 v235, v235, s62, v95
	v_med3_f32 v236, v236, s62, v95
	v_med3_f32 v237, v237, s62, v95
	v_med3_f32 v238, v238, s62, v95
	v_med3_f32 v239, v239, s62, v95
	v_med3_f32 v240, v240, s62, v95
	v_med3_f32 v241, v241, s62, v95
	v_mov_b32_e32 v242, 0
	v_mov_b32_e32 v243, 0
	v_mov_b32_e32 v244, 0
	v_mov_b32_e32 v245, 0
	v_cvt_pk_fp8_f32 v242, v226, v227
	v_cvt_pk_fp8_f32 v243, v230, v231
	v_cvt_pk_fp8_f32 v244, v234, v235
	v_cvt_pk_fp8_f32 v245, v238, v239
	v_cvt_pk_fp8_f32 v242, v228, v229 op_sel:[0,0,1]
	v_cvt_pk_fp8_f32 v243, v232, v233 op_sel:[0,0,1]
	v_cvt_pk_fp8_f32 v244, v236, v237 op_sel:[0,0,1]
	v_cvt_pk_fp8_f32 v245, v240, v241 op_sel:[0,0,1]
	s_nop 0
	global_store_dwordx4 v78, v[242:245], s[6:7]
	s_waitcnt vmcnt(12)
	v_mul_f32_e32 v144, v34, v144
	v_mul_f32_e32 v145, v34, v145
	v_mul_f32_e32 v146, v34, v146
	v_mul_f32_e32 v147, v34, v147
	ds_write_b128 v209, v[144:147]
	v_mul_f32_e32 v148, v35, v148
	v_mul_f32_e32 v149, v35, v149
	v_mul_f32_e32 v150, v35, v150
	v_mul_f32_e32 v151, v35, v151
	ds_write_b128 v209, v[148:151] offset:1024
	v_mul_f32_e32 v152, v36, v152
	v_mul_f32_e32 v153, v36, v153
	v_mul_f32_e32 v154, v36, v154
	v_mul_f32_e32 v155, v36, v155
	ds_write_b128 v209, v[152:155] offset:2048
	v_mul_f32_e32 v156, v37, v156
	v_mul_f32_e32 v157, v37, v157
	v_mul_f32_e32 v158, v37, v158
	v_mul_f32_e32 v159, v37, v159
	ds_write_b128 v209, v[156:159] offset:3072
	v_mul_f32_e32 v160, v38, v160
	v_mul_f32_e32 v161, v38, v161
	v_mul_f32_e32 v162, v38, v162
	v_mul_f32_e32 v163, v38, v163
	ds_write_b128 v209, v[160:163] offset:4096
	v_mul_f32_e32 v164, v39, v164
	v_mul_f32_e32 v165, v39, v165
	v_mul_f32_e32 v166, v39, v166
	v_mul_f32_e32 v167, v39, v167
	ds_write_b128 v209, v[164:167] offset:5120
	v_mul_f32_e32 v168, v40, v168
	v_mul_f32_e32 v169, v40, v169
	v_mul_f32_e32 v170, v40, v170
	v_mul_f32_e32 v171, v40, v171
	ds_write_b128 v209, v[168:171] offset:6144
	v_mul_f32_e32 v172, v41, v172
	v_mul_f32_e32 v173, v41, v173
	v_mul_f32_e32 v174, v41, v174
	v_mul_f32_e32 v175, v41, v175
	ds_write_b128 v209, v[172:175] offset:7168
	s_waitcnt lgkmcnt(0)
	s_barrier
; #define GAS __attribute__((address_space(1)))
; #define LAS __attribute__((address_space(3)))
; #define LDS_WAIT() asm volatile("s_waitcnt lgkmcnt(0)" ::: "memory")
; __device__ __forceinline__ unsigned pk4_fp8(float a, float b, float c, float d) {
;     a = fminf(fmaxf(a, -448.f), 448.f); b = fminf(fmaxf(b, -448.f), 448.f); c = fminf(fmaxf(c, -448.f), 448.f); d = fminf(fmaxf(d, -448.f), 448.f);
;     int w = __builtin_amdgcn_cvt_pk_fp8_f32(a, b, 0, false); w = __builtin_amdgcn_cvt_pk_fp8_f32(c, d, w, true); return (unsigned)w; }
;     const int pr = item >> 1, kb = 2 * (pr / nblk) + (item & 1), nb = pr % nblk, k0 = 64 * kb, n0 = 32 * nb;
;     const int nr = n0 + (lane & 31); const int sc = MAP == 1 ? src_col_in(nr) : nr;
;     float v[32];
; #pragma unroll
;     for (int i = 0; i < 32; ++i) v[i] = sc >= 0 ? W[(size_t)(k0 + 2 * i + (lane >> 5)) * Nsrc + sc] : 0.f;
; #pragma unroll
;     for (int i = 0; i < 32; ++i) { const int k = k0 + 2 * i + (lane >> 5); float x = v[i] * wscale; if (KS) x *= (k < ksplit ? ksA[k] : ksB[k - ksplit]); scr[(2 * i + (lane >> 5)) * 33 + (lane & 31)] = x; }
;     LDS_WAIT(); asm volatile("" ::: "memory");
;     const int c = lane & 7;
; #pragma unroll
;     for (int j = 0; j < 4; ++j) { const int n = (lane >> 3) + 8 * j; const LAS float* s = scr + (8 * c) * 33 + n;
;         const unsigned long long o = (unsigned long long)pg8::pk4_fp8(s[0 * 33], s[1 * 33], s[2 * 33], s[3 * 33]) | ((unsigned long long)pg8::pk4_fp8(s[4 * 33], s[5 * 33], s[6 * 33], s[7 * 33]) << 32);
;         *(GAS unsigned long long*)(WT + (size_t)(n0 + n) * K + k0 + 8 * c) = o; }
;     LDS_WAIT(); asm volatile("" ::: "memory");
; }
	s_add_u32 s8, s34, 0x2000
	s_addc_u32 s9, s35, 0
	global_load_dwordx4 v[144:147], v74, s[8:9]
	s_add_u32 s8, s8, 0x20000
	s_addc_u32 s9, s9, 0
	global_load_dwordx4 v[148:151], v74, s[8:9]
	s_add_u32 s8, s8, 0x20000
	s_addc_u32 s9, s9, 0
	global_load_dwordx4 v[152:155], v74, s[8:9]
	s_add_u32 s8, s8, 0x20000
	s_addc_u32 s9, s9, 0
	global_load_dwordx4 v[156:159], v74, s[8:9]
	s_add_u32 s8, s8, 0x20000
	s_addc_u32 s9, s9, 0
	global_load_dwordx4 v[160:163], v74, s[8:9]
	s_add_u32 s8, s8, 0x20000
	s_addc_u32 s9, s9, 0
	global_load_dwordx4 v[164:167], v74, s[8:9]
	s_add_u32 s8, s8, 0x20000
	s_addc_u32 s9, s9, 0
	global_load_dwordx4 v[168:171], v74, s[8:9]
	s_add_u32 s8, s8, 0x20000
	s_addc_u32 s9, s9, 0
	global_load_dwordx4 v[172:175], v74, s[8:9]
	s_mov_b64 s[6:7], s[36:37]
	ds_read_b32 v226, v211
	ds_read_b32 v227, v211 offset:512
	ds_read_b32 v228, v211 offset:1024
	ds_read_b32 v229, v211 offset:1536
	ds_read_b32 v230, v211 offset:2048
	ds_read_b32 v231, v211 offset:2560
	ds_read_b32 v232, v211 offset:3072
	ds_read_b32 v233, v211 offset:3584
	ds_read_b32 v234, v211 offset:4096
	ds_read_b32 v235, v211 offset:4608
	ds_read_b32 v236, v211 offset:5120
	ds_read_b32 v237, v211 offset:5632
	ds_read_b32 v238, v211 offset:6144
	ds_read_b32 v239, v211 offset:6656
	ds_read_b32 v240, v211 offset:7168
	ds_read_b32 v241, v211 offset:7680
	s_waitcnt lgkmcnt(0)
	v_max_f32_e32 v226, v226, v226
	v_max_f32_e32 v227, v227, v227
	v_max_f32_e32 v228, v228, v228
	v_max_f32_e32 v229, v229, v229
	v_max_f32_e32 v230, v230, v230
	v_max_f32_e32 v231, v231, v231
	v_max_f32_e32 v232, v232, v232
	v_max_f32_e32 v233, v233, v233
	v_max_f32_e32 v234, v234, v234
	v_max_f32_e32 v235, v235, v235
	v_max_f32_e32 v236, v236, v236
	v_max_f32_e32 v237, v237, v237
	v_max_f32_e32 v238, v238, v238
	v_max_f32_e32 v239, v239, v239
	v_max_f32_e32 v240, v240, v240
	v_max_f32_e32 v241, v241, v241
	v_med3_f32 v226, v226, s62, v95
	v_med3_f32 v227, v227, s62, v95
	v_med3_f32 v228, v228, s62, v95
	v_med3_f32 v229, v229, s62, v95
	v_med3_f32 v230, v230, s62, v95
	v_med3_f32 v231, v231, s62, v95
	v_med3_f32 v232, v232, s62, v95
	v_med3_f32 v233, v233, s62, v95
	v_med3_f32 v234, v234, s62, v95
	v_med3_f32 v235, v235, s62, v95
	v_med3_f32 v236, v236, s62, v95
	v_med3_f32 v237, v237, s62, v95
	v_med3_f32 v238, v238, s62, v95
	v_med3_f32 v239, v239, s62, v95
	v_med3_f32 v240, v240, s62, v95
	v_med3_f32 v241, v241, s62, v95
	v_mov_b32_e32 v242, 0
	v_mov_b32_e32 v243, 0
	v_mov_b32_e32 v244, 0
	v_mov_b32_e32 v245, 0
	v_cvt_pk_fp8_f32 v242, v226, v227
	v_cvt_pk_fp8_f32 v243, v230, v231
	v_cvt_pk_fp8_f32 v244, v234, v235
	v_cvt_pk_fp8_f32 v245, v238, v239
	v_cvt_pk_fp8_f32 v242, v228, v229 op_sel:[0,0,1]
	v_cvt_pk_fp8_f32 v243, v232, v233 op_sel:[0,0,1]
	v_cvt_pk_fp8_f32 v244, v236, v237 op_sel:[0,0,1]
	v_cvt_pk_fp8_f32 v245, v240, v241 op_sel:[0,0,1]
	s_nop 0
	global_store_dwordx4 v77, v[242:245], s[6:7]
	ds_read_b32 v226, v213
	ds_read_b32 v227, v213 offset:512
	ds_read_b32 v228, v213 offset:1024
	ds_read_b32 v229, v213 offset:1536
	ds_read_b32 v230, v213 offset:2048
	ds_read_b32 v231, v213 offset:2560
	ds_read_b32 v232, v213 offset:3072
	ds_read_b32 v233, v213 offset:3584
	ds_read_b32 v234, v213 offset:4096
	ds_read_b32 v235, v213 offset:4608
	ds_read_b32 v236, v213 offset:5120
	ds_read_b32 v237, v213 offset:5632
	ds_read_b32 v238, v213 offset:6144
	ds_read_b32 v239, v213 offset:6656
	ds_read_b32 v240, v213 offset:7168
	ds_read_b32 v241, v213 offset:7680
	s_waitcnt lgkmcnt(0)
	v_max_f32_e32 v226, v226, v226
	v_max_f32_e32 v227, v227, v227
	v_max_f32_e32 v228, v228, v228
	v_max_f32_e32 v229, v229, v229
	v_max_f32_e32 v230, v230, v230
	v_max_f32_e32 v231, v231, v231
	v_max_f32_e32 v232, v232, v232
	v_max_f32_e32 v233, v233, v233
	v_max_f32_e32 v234, v234, v234
	v_max_f32_e32 v235, v235, v235
	v_max_f32_e32 v236, v236, v236
	v_max_f32_e32 v237, v237, v237
	v_max_f32_e32 v238, v238, v238
	v_max_f32_e32 v239, v239, v239
	v_max_f32_e32 v240, v240, v240
	v_max_f32_e32 v241, v241, v241
	v_med3_f32 v226, v226, s62, v95
	v_med3_f32 v227, v227, s62, v95
	v_med3_f32 v228, v228, s62, v95
	v_med3_f32 v229, v229, s62, v95
	v_med3_f32 v230, v230, s62, v95
	v_med3_f32 v231, v231, s62, v95
	v_med3_f32 v232, v232, s62, v95
	v_med3_f32 v233, v233, s62, v95
	v_med3_f32 v234, v234, s62, v95
	v_med3_f32 v235, v235, s62, v95
	v_med3_f32 v236, v236, s62, v95
	v_med3_f32 v237, v237, s62, v95
	v_med3_f32 v238, v238, s62, v95
	v_med3_f32 v239, v239, s62, v95
	v_med3_f32 v240, v240, s62, v95
	v_med3_f32 v241, v241, s62, v95
	v_mov_b32_e32 v242, 0
	v_mov_b32_e32 v243, 0
	v_mov_b32_e32 v244, 0
	v_mov_b32_e32 v245, 0
	v_cvt_pk_fp8_f32 v242, v226, v227
	v_cvt_pk_fp8_f32 v243, v230, v231
	v_cvt_pk_fp8_f32 v244, v234, v235
	v_cvt_pk_fp8_f32 v245, v238, v239
	v_cvt_pk_fp8_f32 v242, v228, v229 op_sel:[0,0,1]
	v_cvt_pk_fp8_f32 v243, v232, v233 op_sel:[0,0,1]
	v_cvt_pk_fp8_f32 v244, v236, v237 op_sel:[0,0,1]
	v_cvt_pk_fp8_f32 v245, v240, v241 op_sel:[0,0,1]
	s_nop 0
	global_store_dwordx4 v78, v[242:245], s[6:7]
	s_waitcnt vmcnt(12)
	v_mul_f32_e32 v176, v34, v176
	v_mul_f32_e32 v177, v34, v177
	v_mul_f32_e32 v178, v34, v178
	v_mul_f32_e32 v179, v34, v179
	ds_write_b128 v210, v[176:179]
	v_mul_f32_e32 v180, v35, v180
	v_mul_f32_e32 v181, v35, v181
	v_mul_f32_e32 v182, v35, v182
	v_mul_f32_e32 v183, v35, v183
	ds_write_b128 v210, v[180:183] offset:1024
	v_mul_f32_e32 v184, v36, v184
	v_mul_f32_e32 v185, v36, v185
	v_mul_f32_e32 v186, v36, v186
	v_mul_f32_e32 v187, v36, v187
	ds_write_b128 v210, v[184:187] offset:2048
	v_mul_f32_e32 v188, v37, v188
	v_mul_f32_e32 v189, v37, v189
	v_mul_f32_e32 v190, v37, v190
	v_mul_f32_e32 v191, v37, v191
	ds_write_b128 v210, v[188:191] offset:3072
	v_mul_f32_e32 v192, v38, v192
	v_mul_f32_e32 v193, v38, v193
	v_mul_f32_e32 v194, v38, v194
	v_mul_f32_e32 v195, v38, v195
	ds_write_b128 v210, v[192:195] offset:4096
	v_mul_f32_e32 v196, v39, v196
	v_mul_f32_e32 v197, v39, v197
	v_mul_f32_e32 v198, v39, v198
	v_mul_f32_e32 v199, v39, v199
	ds_write_b128 v210, v[196:199] offset:5120
	v_mul_f32_e32 v200, v40, v200
	v_mul_f32_e32 v201, v40, v201
	v_mul_f32_e32 v202, v40, v202
	v_mul_f32_e32 v203, v40, v203
	ds_write_b128 v210, v[200:203] offset:6144
	v_mul_f32_e32 v204, v41, v204
	v_mul_f32_e32 v205, v41, v205
	v_mul_f32_e32 v206, v41, v206
	v_mul_f32_e32 v207, v41, v207
	ds_write_b128 v210, v[204:207] offset:7168
	s_waitcnt lgkmcnt(0)
	s_barrier
; #define GAS __attribute__((address_space(1)))
; #define LAS __attribute__((address_space(3)))
; #define LDS_WAIT() asm volatile("s_waitcnt lgkmcnt(0)" ::: "memory")
; __device__ __forceinline__ unsigned pk4_fp8(float a, float b, float c, float d) {
;     a = fminf(fmaxf(a, -448.f), 448.f); b = fminf(fmaxf(b, -448.f), 448.f); c = fminf(fmaxf(c, -448.f), 448.f); d = fminf(fmaxf(d, -448.f), 448.f);
;     int w = __builtin_amdgcn_cvt_pk_fp8_f32(a, b, 0, false); w = __builtin_amdgcn_cvt_pk_fp8_f32(c, d, w, true); return (unsigned)w; }
;     const int pr = item >> 1, kb = 2 * (pr / nblk) + (item & 1), nb = pr % nblk, k0 = 64 * kb, n0 = 32 * nb;
;     const int nr = n0 + (lane & 31); const int sc = MAP == 1 ? src_col_in(nr) : nr;
;     float v[32];
; #pragma unroll
;     for (int i = 0; i < 32; ++i) v[i] = sc >= 0 ? W[(size_t)(k0 + 2 * i + (lane >> 5)) * Nsrc + sc] : 0.f;
; #pragma unroll
;     for (int i = 0; i < 32; ++i) { const int k = k0 + 2 * i + (lane >> 5); float x = v[i] * wscale; if (KS) x *= (k < ksplit ? ksA[k] : ksB[k - ksplit]); scr[(2 * i + (lane >> 5)) * 33 + (lane & 31)] = x; }
;     LDS_WAIT(); asm volatile("" ::: "memory");
;     const int c = lane & 7;
; #pragma unroll
;     for (int j = 0; j < 4; ++j) { const int n = (lane >> 3) + 8 * j; const LAS float* s = scr + (8 * c) * 33 + n;
;         const unsigned long long o = (unsigned long long)pg8::pk4_fp8(s[0 * 33], s[1 * 33], s[2 * 33], s[3 * 33]) | ((unsigned long long)pg8::pk4_fp8(s[4 * 33], s[5 * 33], s[6 * 33], s[7 * 33]) << 32);
;         *(GAS unsigned long long*)(WT + (size_t)(n0 + n) * K + k0 + 8 * c) = o; }
;     LDS_WAIT(); asm volatile("" ::: "memory");
; }
	s_add_u32 s8, s34, 0x3000
	s_addc_u32 s9, s35, 0
	global_load_dwordx4 v[176:179], v74, s[8:9]
	s_add_u32 s8, s8, 0x20000
	s_addc_u32 s9, s9, 0
	global_load_dwordx4 v[180:183], v74, s[8:9]
	s_add_u32 s8, s8, 0x20000
	s_addc_u32 s9, s9, 0
	global_load_dwordx4 v[184:187], v74, s[8:9]
	s_add_u32 s8, s8, 0x20000
	s_addc_u32 s9, s9, 0
	global_load_dwordx4 v[188:191], v74, s[8:9]
	s_add_u32 s8, s8, 0x20000
	s_addc_u32 s9, s9, 0
	global_load_dwordx4 v[192:195], v74, s[8:9]
	s_add_u32 s8, s8, 0x20000
	s_addc_u32 s9, s9, 0
	global_load_dwordx4 v[196:199], v74, s[8:9]
	s_add_u32 s8, s8, 0x20000
	s_addc_u32 s9, s9, 0
	global_load_dwordx4 v[200:203], v74, s[8:9]
	s_add_u32 s8, s8, 0x20000
	s_addc_u32 s9, s9, 0
	global_load_dwordx4 v[204:207], v74, s[8:9]
	s_add_u32 s6, s36, 0x400000
	s_addc_u32 s7, s37, 0
	ds_read_b32 v226, v212
	ds_read_b32 v227, v212 offset:512
	ds_read_b32 v228, v212 offset:1024
	ds_read_b32 v229, v212 offset:1536
	ds_read_b32 v230, v212 offset:2048
	ds_read_b32 v231, v212 offset:2560
	ds_read_b32 v232, v212 offset:3072
	ds_read_b32 v233, v212 offset:3584
	ds_read_b32 v234, v212 offset:4096
	ds_read_b32 v235, v212 offset:4608
	ds_read_b32 v236, v212 offset:5120
	ds_read_b32 v237, v212 offset:5632
	ds_read_b32 v238, v212 offset:6144
	ds_read_b32 v239, v212 offset:6656
	ds_read_b32 v240, v212 offset:7168
	ds_read_b32 v241, v212 offset:7680
	s_waitcnt lgkmcnt(0)
	v_max_f32_e32 v226, v226, v226
	v_max_f32_e32 v227, v227, v227
	v_max_f32_e32 v228, v228, v228
	v_max_f32_e32 v229, v229, v229
	v_max_f32_e32 v230, v230, v230
	v_max_f32_e32 v231, v231, v231
	v_max_f32_e32 v232, v232, v232
	v_max_f32_e32 v233, v233, v233
	v_max_f32_e32 v234, v234, v234
	v_max_f32_e32 v235, v235, v235
	v_max_f32_e32 v236, v236, v236
	v_max_f32_e32 v237, v237, v237
	v_max_f32_e32 v238, v238, v238
	v_max_f32_e32 v239, v239, v239
	v_max_f32_e32 v240, v240, v240
	v_max_f32_e32 v241, v241, v241
	v_med3_f32 v226, v226, s62, v95
	v_med3_f32 v227, v227, s62, v95
	v_med3_f32 v228, v228, s62, v95
	v_med3_f32 v229, v229, s62, v95
	v_med3_f32 v230, v230, s62, v95
	v_med3_f32 v231, v231, s62, v95
	v_med3_f32 v232, v232, s62, v95
	v_med3_f32 v233, v233, s62, v95
	v_med3_f32 v234, v234, s62, v95
	v_med3_f32 v235, v235, s62, v95
	v_med3_f32 v236, v236, s62, v95
	v_med3_f32 v237, v237, s62, v95
	v_med3_f32 v238, v238, s62, v95
	v_med3_f32 v239, v239, s62, v95
	v_med3_f32 v240, v240, s62, v95
	v_med3_f32 v241, v241, s62, v95
	v_mov_b32_e32 v242, 0
	v_mov_b32_e32 v243, 0
	v_mov_b32_e32 v244, 0
	v_mov_b32_e32 v245, 0
	v_cvt_pk_fp8_f32 v242, v226, v227
	v_cvt_pk_fp8_f32 v243, v230, v231
	v_cvt_pk_fp8_f32 v244, v234, v235
	v_cvt_pk_fp8_f32 v245, v238, v239
	v_cvt_pk_fp8_f32 v242, v228, v229 op_sel:[0,0,1]
	v_cvt_pk_fp8_f32 v243, v232, v233 op_sel:[0,0,1]
	v_cvt_pk_fp8_f32 v244, v236, v237 op_sel:[0,0,1]
	v_cvt_pk_fp8_f32 v245, v240, v241 op_sel:[0,0,1]
	s_nop 0
	global_store_dwordx4 v77, v[242:245], s[6:7]
	ds_read_b32 v226, v214
	ds_read_b32 v227, v214 offset:512
	ds_read_b32 v228, v214 offset:1024
	ds_read_b32 v229, v214 offset:1536
	ds_read_b32 v230, v214 offset:2048
	ds_read_b32 v231, v214 offset:2560
	ds_read_b32 v232, v214 offset:3072
	ds_read_b32 v233, v214 offset:3584
	ds_read_b32 v234, v214 offset:4096
	ds_read_b32 v235, v214 offset:4608
	ds_read_b32 v236, v214 offset:5120
	ds_read_b32 v237, v214 offset:5632
	ds_read_b32 v238, v214 offset:6144
	ds_read_b32 v239, v214 offset:6656
	ds_read_b32 v240, v214 offset:7168
	ds_read_b32 v241, v214 offset:7680
	s_waitcnt lgkmcnt(0)
	v_max_f32_e32 v226, v226, v226
	v_max_f32_e32 v227, v227, v227
	v_max_f32_e32 v228, v228, v228
	v_max_f32_e32 v229, v229, v229
	v_max_f32_e32 v230, v230, v230
	v_max_f32_e32 v231, v231, v231
	v_max_f32_e32 v232, v232, v232
	v_max_f32_e32 v233, v233, v233
	v_max_f32_e32 v234, v234, v234
	v_max_f32_e32 v235, v235, v235
	v_max_f32_e32 v236, v236, v236
	v_max_f32_e32 v237, v237, v237
	v_max_f32_e32 v238, v238, v238
	v_max_f32_e32 v239, v239, v239
	v_max_f32_e32 v240, v240, v240
	v_max_f32_e32 v241, v241, v241
	v_med3_f32 v226, v226, s62, v95
	v_med3_f32 v227, v227, s62, v95
	v_med3_f32 v228, v228, s62, v95
	v_med3_f32 v229, v229, s62, v95
	v_med3_f32 v230, v230, s62, v95
	v_med3_f32 v231, v231, s62, v95
	v_med3_f32 v232, v232, s62, v95
	v_med3_f32 v233, v233, s62, v95
	v_med3_f32 v234, v234, s62, v95
	v_med3_f32 v235, v235, s62, v95
	v_med3_f32 v236, v236, s62, v95
	v_med3_f32 v237, v237, s62, v95
	v_med3_f32 v238, v238, s62, v95
	v_med3_f32 v239, v239, s62, v95
	v_med3_f32 v240, v240, s62, v95
	v_med3_f32 v241, v241, s62, v95
	v_mov_b32_e32 v242, 0
	v_mov_b32_e32 v243, 0
	v_mov_b32_e32 v244, 0
	v_mov_b32_e32 v245, 0
	v_cvt_pk_fp8_f32 v242, v226, v227
	v_cvt_pk_fp8_f32 v243, v230, v231
	v_cvt_pk_fp8_f32 v244, v234, v235
	v_cvt_pk_fp8_f32 v245, v238, v239
	v_cvt_pk_fp8_f32 v242, v228, v229 op_sel:[0,0,1]
	v_cvt_pk_fp8_f32 v243, v232, v233 op_sel:[0,0,1]
	v_cvt_pk_fp8_f32 v244, v236, v237 op_sel:[0,0,1]
	v_cvt_pk_fp8_f32 v245, v240, v241 op_sel:[0,0,1]
	s_nop 0
	global_store_dwordx4 v78, v[242:245], s[6:7]
	s_waitcnt vmcnt(12)
	v_mul_f32_e32 v144, v34, v144
	v_mul_f32_e32 v145, v34, v145
	v_mul_f32_e32 v146, v34, v146
	v_mul_f32_e32 v147, v34, v147
	ds_write_b128 v209, v[144:147]
	v_mul_f32_e32 v148, v35, v148
	v_mul_f32_e32 v149, v35, v149
	v_mul_f32_e32 v150, v35, v150
	v_mul_f32_e32 v151, v35, v151
	ds_write_b128 v209, v[148:151] offset:1024
	v_mul_f32_e32 v152, v36, v152
	v_mul_f32_e32 v153, v36, v153
	v_mul_f32_e32 v154, v36, v154
	v_mul_f32_e32 v155, v36, v155
	ds_write_b128 v209, v[152:155] offset:2048
	v_mul_f32_e32 v156, v37, v156
	v_mul_f32_e32 v157, v37, v157
	v_mul_f32_e32 v158, v37, v158
	v_mul_f32_e32 v159, v37, v159
	ds_write_b128 v209, v[156:159] offset:3072
	v_mul_f32_e32 v160, v38, v160
	v_mul_f32_e32 v161, v38, v161
	v_mul_f32_e32 v162, v38, v162
	v_mul_f32_e32 v163, v38, v163
	ds_write_b128 v209, v[160:163] offset:4096
	v_mul_f32_e32 v164, v39, v164
	v_mul_f32_e32 v165, v39, v165
	v_mul_f32_e32 v166, v39, v166
	v_mul_f32_e32 v167, v39, v167
	ds_write_b128 v209, v[164:167] offset:5120
	v_mul_f32_e32 v168, v40, v168
	v_mul_f32_e32 v169, v40, v169
	v_mul_f32_e32 v170, v40, v170
	v_mul_f32_e32 v171, v40, v171
	ds_write_b128 v209, v[168:171] offset:6144
	v_mul_f32_e32 v172, v41, v172
	v_mul_f32_e32 v173, v41, v173
	v_mul_f32_e32 v174, v41, v174
	v_mul_f32_e32 v175, v41, v175
	ds_write_b128 v209, v[172:175] offset:7168
	s_waitcnt lgkmcnt(0)
	s_barrier
; #define GAS __attribute__((address_space(1)))
; #define LAS __attribute__((address_space(3)))
; #define LDS_WAIT() asm volatile("s_waitcnt lgkmcnt(0)" ::: "memory")
; __device__ __forceinline__ unsigned pk4_fp8(float a, float b, float c, float d) {
;     a = fminf(fmaxf(a, -448.f), 448.f); b = fminf(fmaxf(b, -448.f), 448.f); c = fminf(fmaxf(c, -448.f), 448.f); d = fminf(fmaxf(d, -448.f), 448.f);
;     int w = __builtin_amdgcn_cvt_pk_fp8_f32(a, b, 0, false); w = __builtin_amdgcn_cvt_pk_fp8_f32(c, d, w, true); return (unsigned)w; }
;     const int pr = item >> 1, kb = 2 * (pr / nblk) + (item & 1), nb = pr % nblk, k0 = 64 * kb, n0 = 32 * nb;
;     const int nr = n0 + (lane & 31); const int sc = MAP == 1 ? src_col_in(nr) : nr;
;     float v[32];
; #pragma unroll
;     for (int i = 0; i < 32; ++i) v[i] = sc >= 0 ? W[(size_t)(k0 + 2 * i + (lane >> 5)) * Nsrc + sc] : 0.f;
; #pragma unroll
;     for (int i = 0; i < 32; ++i) { const int k = k0 + 2 * i + (lane >> 5); float x = v[i] * wscale; if (KS) x *= (k < ksplit ? ksA[k] : ksB[k - ksplit]); scr[(2 * i + (lane >> 5)) * 33 + (lane & 31)] = x; }
;     LDS_WAIT(); asm volatile("" ::: "memory");
;     const int c = lane & 7;
; #pragma unroll
;     for (int j = 0; j < 4; ++j) { const int n = (lane >> 3) + 8 * j; const LAS float* s = scr + (8 * c) * 33 + n;
;         const unsigned long long o = (unsigned long long)pg8::pk4_fp8(s[0 * 33], s[1 * 33], s[2 * 33], s[3 * 33]) | ((unsigned long long)pg8::pk4_fp8(s[4 * 33], s[5 * 33], s[6 * 33], s[7 * 33]) << 32);
;         *(GAS unsigned long long*)(WT + (size_t)(n0 + n) * K + k0 + 8 * c) = o; }
;     LDS_WAIT(); asm volatile("" ::: "memory");
; }
	s_add_u32 s8, s34, 0x4000
	s_addc_u32 s9, s35, 0
	global_load_dwordx4 v[144:147], v74, s[8:9]
	s_add_u32 s8, s8, 0x20000
	s_addc_u32 s9, s9, 0
	global_load_dwordx4 v[148:151], v74, s[8:9]
	s_add_u32 s8, s8, 0x20000
	s_addc_u32 s9, s9, 0
	global_load_dwordx4 v[152:155], v74, s[8:9]
	s_add_u32 s8, s8, 0x20000
	s_addc_u32 s9, s9, 0
	global_load_dwordx4 v[156:159], v74, s[8:9]
	s_add_u32 s8, s8, 0x20000
	s_addc_u32 s9, s9, 0
	global_load_dwordx4 v[160:163], v74, s[8:9]
	s_add_u32 s8, s8, 0x20000
	s_addc_u32 s9, s9, 0
	global_load_dwordx4 v[164:167], v74, s[8:9]
	s_add_u32 s8, s8, 0x20000
	s_addc_u32 s9, s9, 0
	global_load_dwordx4 v[168:171], v74, s[8:9]
	s_add_u32 s8, s8, 0x20000
	s_addc_u32 s9, s9, 0
	global_load_dwordx4 v[172:175], v74, s[8:9]
	s_add_u32 s6, s36, 0x800000
	s_addc_u32 s7, s37, 0
	ds_read_b32 v226, v211
	ds_read_b32 v227, v211 offset:512
	ds_read_b32 v228, v211 offset:1024
	ds_read_b32 v229, v211 offset:1536
	ds_read_b32 v230, v211 offset:2048
	ds_read_b32 v231, v211 offset:2560
	ds_read_b32 v232, v211 offset:3072
	ds_read_b32 v233, v211 offset:3584
	ds_read_b32 v234, v211 offset:4096
	ds_read_b32 v235, v211 offset:4608
	ds_read_b32 v236, v211 offset:5120
	ds_read_b32 v237, v211 offset:5632
	ds_read_b32 v238, v211 offset:6144
	ds_read_b32 v239, v211 offset:6656
	ds_read_b32 v240, v211 offset:7168
	ds_read_b32 v241, v211 offset:7680
	s_waitcnt lgkmcnt(0)
	v_max_f32_e32 v226, v226, v226
	v_max_f32_e32 v227, v227, v227
	v_max_f32_e32 v228, v228, v228
	v_max_f32_e32 v229, v229, v229
	v_max_f32_e32 v230, v230, v230
	v_max_f32_e32 v231, v231, v231
	v_max_f32_e32 v232, v232, v232
	v_max_f32_e32 v233, v233, v233
	v_max_f32_e32 v234, v234, v234
	v_max_f32_e32 v235, v235, v235
	v_max_f32_e32 v236, v236, v236
	v_max_f32_e32 v237, v237, v237
	v_max_f32_e32 v238, v238, v238
	v_max_f32_e32 v239, v239, v239
	v_max_f32_e32 v240, v240, v240
	v_max_f32_e32 v241, v241, v241
	v_med3_f32 v226, v226, s62, v95
	v_med3_f32 v227, v227, s62, v95
	v_med3_f32 v228, v228, s62, v95
	v_med3_f32 v229, v229, s62, v95
	v_med3_f32 v230, v230, s62, v95
	v_med3_f32 v231, v231, s62, v95
	v_med3_f32 v232, v232, s62, v95
	v_med3_f32 v233, v233, s62, v95
	v_med3_f32 v234, v234, s62, v95
	v_med3_f32 v235, v235, s62, v95
	v_med3_f32 v236, v236, s62, v95
	v_med3_f32 v237, v237, s62, v95
	v_med3_f32 v238, v238, s62, v95
	v_med3_f32 v239, v239, s62, v95
	v_med3_f32 v240, v240, s62, v95
	v_med3_f32 v241, v241, s62, v95
	v_mov_b32_e32 v242, 0
	v_mov_b32_e32 v243, 0
	v_mov_b32_e32 v244, 0
	v_mov_b32_e32 v245, 0
	v_cvt_pk_fp8_f32 v242, v226, v227
	v_cvt_pk_fp8_f32 v243, v230, v231
	v_cvt_pk_fp8_f32 v244, v234, v235
	v_cvt_pk_fp8_f32 v245, v238, v239
	v_cvt_pk_fp8_f32 v242, v228, v229 op_sel:[0,0,1]
	v_cvt_pk_fp8_f32 v243, v232, v233 op_sel:[0,0,1]
	v_cvt_pk_fp8_f32 v244, v236, v237 op_sel:[0,0,1]
	v_cvt_pk_fp8_f32 v245, v240, v241 op_sel:[0,0,1]
	s_nop 0
	global_store_dwordx4 v77, v[242:245], s[6:7]
	ds_read_b32 v226, v213
	ds_read_b32 v227, v213 offset:512
	ds_read_b32 v228, v213 offset:1024
	ds_read_b32 v229, v213 offset:1536
	ds_read_b32 v230, v213 offset:2048
	ds_read_b32 v231, v213 offset:2560
	ds_read_b32 v232, v213 offset:3072
	ds_read_b32 v233, v213 offset:3584
	ds_read_b32 v234, v213 offset:4096
	ds_read_b32 v235, v213 offset:4608
	ds_read_b32 v236, v213 offset:5120
	ds_read_b32 v237, v213 offset:5632
	ds_read_b32 v238, v213 offset:6144
	ds_read_b32 v239, v213 offset:6656
	ds_read_b32 v240, v213 offset:7168
	ds_read_b32 v241, v213 offset:7680
	s_waitcnt lgkmcnt(0)
	v_max_f32_e32 v226, v226, v226
	v_max_f32_e32 v227, v227, v227
	v_max_f32_e32 v228, v228, v228
	v_max_f32_e32 v229, v229, v229
	v_max_f32_e32 v230, v230, v230
	v_max_f32_e32 v231, v231, v231
	v_max_f32_e32 v232, v232, v232
	v_max_f32_e32 v233, v233, v233
	v_max_f32_e32 v234, v234, v234
	v_max_f32_e32 v235, v235, v235
	v_max_f32_e32 v236, v236, v236
	v_max_f32_e32 v237, v237, v237
	v_max_f32_e32 v238, v238, v238
	v_max_f32_e32 v239, v239, v239
	v_max_f32_e32 v240, v240, v240
	v_max_f32_e32 v241, v241, v241
	v_med3_f32 v226, v226, s62, v95
	v_med3_f32 v227, v227, s62, v95
	v_med3_f32 v228, v228, s62, v95
	v_med3_f32 v229, v229, s62, v95
	v_med3_f32 v230, v230, s62, v95
	v_med3_f32 v231, v231, s62, v95
	v_med3_f32 v232, v232, s62, v95
	v_med3_f32 v233, v233, s62, v95
	v_med3_f32 v234, v234, s62, v95
	v_med3_f32 v235, v235, s62, v95
	v_med3_f32 v236, v236, s62, v95
	v_med3_f32 v237, v237, s62, v95
	v_med3_f32 v238, v238, s62, v95
	v_med3_f32 v239, v239, s62, v95
	v_med3_f32 v240, v240, s62, v95
	v_med3_f32 v241, v241, s62, v95
	v_mov_b32_e32 v242, 0
	v_mov_b32_e32 v243, 0
	v_mov_b32_e32 v244, 0
	v_mov_b32_e32 v245, 0
	v_cvt_pk_fp8_f32 v242, v226, v227
	v_cvt_pk_fp8_f32 v243, v230, v231
	v_cvt_pk_fp8_f32 v244, v234, v235
	v_cvt_pk_fp8_f32 v245, v238, v239
	v_cvt_pk_fp8_f32 v242, v228, v229 op_sel:[0,0,1]
	v_cvt_pk_fp8_f32 v243, v232, v233 op_sel:[0,0,1]
	v_cvt_pk_fp8_f32 v244, v236, v237 op_sel:[0,0,1]
	v_cvt_pk_fp8_f32 v245, v240, v241 op_sel:[0,0,1]
	s_nop 0
	global_store_dwordx4 v78, v[242:245], s[6:7]
	s_waitcnt vmcnt(12)
	v_mul_f32_e32 v176, v34, v176
	v_mul_f32_e32 v177, v34, v177
	v_mul_f32_e32 v178, v34, v178
	v_mul_f32_e32 v179, v34, v179
	ds_write_b128 v210, v[176:179]
	v_mul_f32_e32 v180, v35, v180
	v_mul_f32_e32 v181, v35, v181
	v_mul_f32_e32 v182, v35, v182
	v_mul_f32_e32 v183, v35, v183
	ds_write_b128 v210, v[180:183] offset:1024
	v_mul_f32_e32 v184, v36, v184
	v_mul_f32_e32 v185, v36, v185
	v_mul_f32_e32 v186, v36, v186
	v_mul_f32_e32 v187, v36, v187
	ds_write_b128 v210, v[184:187] offset:2048
	v_mul_f32_e32 v188, v37, v188
	v_mul_f32_e32 v189, v37, v189
	v_mul_f32_e32 v190, v37, v190
	v_mul_f32_e32 v191, v37, v191
	ds_write_b128 v210, v[188:191] offset:3072
	v_mul_f32_e32 v192, v38, v192
	v_mul_f32_e32 v193, v38, v193
	v_mul_f32_e32 v194, v38, v194
	v_mul_f32_e32 v195, v38, v195
	ds_write_b128 v210, v[192:195] offset:4096
	v_mul_f32_e32 v196, v39, v196
	v_mul_f32_e32 v197, v39, v197
	v_mul_f32_e32 v198, v39, v198
	v_mul_f32_e32 v199, v39, v199
	ds_write_b128 v210, v[196:199] offset:5120
	v_mul_f32_e32 v200, v40, v200
	v_mul_f32_e32 v201, v40, v201
	v_mul_f32_e32 v202, v40, v202
	v_mul_f32_e32 v203, v40, v203
	ds_write_b128 v210, v[200:203] offset:6144
	v_mul_f32_e32 v204, v41, v204
	v_mul_f32_e32 v205, v41, v205
	v_mul_f32_e32 v206, v41, v206
	v_mul_f32_e32 v207, v41, v207
	ds_write_b128 v210, v[204:207] offset:7168
	s_waitcnt lgkmcnt(0)
	s_barrier
; #define GAS __attribute__((address_space(1)))
; #define LAS __attribute__((address_space(3)))
; #define LDS_WAIT() asm volatile("s_waitcnt lgkmcnt(0)" ::: "memory")
; __device__ __forceinline__ unsigned pk4_fp8(float a, float b, float c, float d) {
;     a = fminf(fmaxf(a, -448.f), 448.f); b = fminf(fmaxf(b, -448.f), 448.f); c = fminf(fmaxf(c, -448.f), 448.f); d = fminf(fmaxf(d, -448.f), 448.f);
;     int w = __builtin_amdgcn_cvt_pk_fp8_f32(a, b, 0, false); w = __builtin_amdgcn_cvt_pk_fp8_f32(c, d, w, true); return (unsigned)w; }
;     const int pr = item >> 1, kb = 2 * (pr / nblk) + (item & 1), nb = pr % nblk, k0 = 64 * kb, n0 = 32 * nb;
;     const int nr = n0 + (lane & 31); const int sc = MAP == 1 ? src_col_in(nr) : nr;
;     float v[32];
; #pragma unroll
;     for (int i = 0; i < 32; ++i) v[i] = sc >= 0 ? W[(size_t)(k0 + 2 * i + (lane >> 5)) * Nsrc + sc] : 0.f;
; #pragma unroll
;     for (int i = 0; i < 32; ++i) { const int k = k0 + 2 * i + (lane >> 5); float x = v[i] * wscale; if (KS) x *= (k < ksplit ? ksA[k] : ksB[k - ksplit]); scr[(2 * i + (lane >> 5)) * 33 + (lane & 31)] = x; }
;     LDS_WAIT(); asm volatile("" ::: "memory");
;     const int c = lane & 7;
; #pragma unroll
;     for (int j = 0; j < 4; ++j) { const int n = (lane >> 3) + 8 * j; const LAS float* s = scr + (8 * c) * 33 + n;
;         const unsigned long long o = (unsigned long long)pg8::pk4_fp8(s[0 * 33], s[1 * 33], s[2 * 33], s[3 * 33]) | ((unsigned long long)pg8::pk4_fp8(s[4 * 33], s[5 * 33], s[6 * 33], s[7 * 33]) << 32);
;         *(GAS unsigned long long*)(WT + (size_t)(n0 + n) * K + k0 + 8 * c) = o; }
;     LDS_WAIT(); asm volatile("" ::: "memory");
; }
	s_add_u32 s8, s34, 0x5000
	s_addc_u32 s9, s35, 0
	global_load_dwordx4 v[176:179], v74, s[8:9]
	s_add_u32 s8, s8, 0x20000
	s_addc_u32 s9, s9, 0
	global_load_dwordx4 v[180:183], v74, s[8:9]
	s_add_u32 s8, s8, 0x20000
	s_addc_u32 s9, s9, 0
	global_load_dwordx4 v[184:187], v74, s[8:9]
	s_add_u32 s8, s8, 0x20000
	s_addc_u32 s9, s9, 0
	global_load_dwordx4 v[188:191], v74, s[8:9]
	s_add_u32 s8, s8, 0x20000
	s_addc_u32 s9, s9, 0
	global_load_dwordx4 v[192:195], v74, s[8:9]
	s_add_u32 s8, s8, 0x20000
	s_addc_u32 s9, s9, 0
	global_load_dwordx4 v[196:199], v74, s[8:9]
	s_add_u32 s8, s8, 0x20000
	s_addc_u32 s9, s9, 0
	global_load_dwordx4 v[200:203], v74, s[8:9]
	s_add_u32 s8, s8, 0x20000
	s_addc_u32 s9, s9, 0
	global_load_dwordx4 v[204:207], v74, s[8:9]
	s_add_u32 s6, s36, 0xc00000
	s_addc_u32 s7, s37, 0
	ds_read_b32 v226, v212
	ds_read_b32 v227, v212 offset:512
	ds_read_b32 v228, v212 offset:1024
	ds_read_b32 v229, v212 offset:1536
	ds_read_b32 v230, v212 offset:2048
	ds_read_b32 v231, v212 offset:2560
	ds_read_b32 v232, v212 offset:3072
	ds_read_b32 v233, v212 offset:3584
	ds_read_b32 v234, v212 offset:4096
	ds_read_b32 v235, v212 offset:4608
	ds_read_b32 v236, v212 offset:5120
	ds_read_b32 v237, v212 offset:5632
	ds_read_b32 v238, v212 offset:6144
	ds_read_b32 v239, v212 offset:6656
	ds_read_b32 v240, v212 offset:7168
	ds_read_b32 v241, v212 offset:7680
	s_waitcnt lgkmcnt(0)
	v_max_f32_e32 v226, v226, v226
	v_max_f32_e32 v227, v227, v227
	v_max_f32_e32 v228, v228, v228
	v_max_f32_e32 v229, v229, v229
	v_max_f32_e32 v230, v230, v230
	v_max_f32_e32 v231, v231, v231
	v_max_f32_e32 v232, v232, v232
	v_max_f32_e32 v233, v233, v233
	v_max_f32_e32 v234, v234, v234
	v_max_f32_e32 v235, v235, v235
	v_max_f32_e32 v236, v236, v236
	v_max_f32_e32 v237, v237, v237
	v_max_f32_e32 v238, v238, v238
	v_max_f32_e32 v239, v239, v239
	v_max_f32_e32 v240, v240, v240
	v_max_f32_e32 v241, v241, v241
	v_med3_f32 v226, v226, s62, v95
	v_med3_f32 v227, v227, s62, v95
	v_med3_f32 v228, v228, s62, v95
	v_med3_f32 v229, v229, s62, v95
	v_med3_f32 v230, v230, s62, v95
	v_med3_f32 v231, v231, s62, v95
	v_med3_f32 v232, v232, s62, v95
	v_med3_f32 v233, v233, s62, v95
	v_med3_f32 v234, v234, s62, v95
	v_med3_f32 v235, v235, s62, v95
	v_med3_f32 v236, v236, s62, v95
	v_med3_f32 v237, v237, s62, v95
	v_med3_f32 v238, v238, s62, v95
	v_med3_f32 v239, v239, s62, v95
	v_med3_f32 v240, v240, s62, v95
	v_med3_f32 v241, v241, s62, v95
	v_mov_b32_e32 v242, 0
	v_mov_b32_e32 v243, 0
	v_mov_b32_e32 v244, 0
	v_mov_b32_e32 v245, 0
	v_cvt_pk_fp8_f32 v242, v226, v227
	v_cvt_pk_fp8_f32 v243, v230, v231
	v_cvt_pk_fp8_f32 v244, v234, v235
	v_cvt_pk_fp8_f32 v245, v238, v239
	v_cvt_pk_fp8_f32 v242, v228, v229 op_sel:[0,0,1]
	v_cvt_pk_fp8_f32 v243, v232, v233 op_sel:[0,0,1]
	v_cvt_pk_fp8_f32 v244, v236, v237 op_sel:[0,0,1]
	v_cvt_pk_fp8_f32 v245, v240, v241 op_sel:[0,0,1]
	s_nop 0
	global_store_dwordx4 v77, v[242:245], s[6:7]
	ds_read_b32 v226, v214
	ds_read_b32 v227, v214 offset:512
	ds_read_b32 v228, v214 offset:1024
	ds_read_b32 v229, v214 offset:1536
	ds_read_b32 v230, v214 offset:2048
	ds_read_b32 v231, v214 offset:2560
	ds_read_b32 v232, v214 offset:3072
	ds_read_b32 v233, v214 offset:3584
	ds_read_b32 v234, v214 offset:4096
	ds_read_b32 v235, v214 offset:4608
	ds_read_b32 v236, v214 offset:5120
	ds_read_b32 v237, v214 offset:5632
	ds_read_b32 v238, v214 offset:6144
	ds_read_b32 v239, v214 offset:6656
	ds_read_b32 v240, v214 offset:7168
	ds_read_b32 v241, v214 offset:7680
	s_waitcnt lgkmcnt(0)
	v_max_f32_e32 v226, v226, v226
	v_max_f32_e32 v227, v227, v227
	v_max_f32_e32 v228, v228, v228
	v_max_f32_e32 v229, v229, v229
	v_max_f32_e32 v230, v230, v230
	v_max_f32_e32 v231, v231, v231
	v_max_f32_e32 v232, v232, v232
	v_max_f32_e32 v233, v233, v233
	v_max_f32_e32 v234, v234, v234
	v_max_f32_e32 v235, v235, v235
	v_max_f32_e32 v236, v236, v236
	v_max_f32_e32 v237, v237, v237
	v_max_f32_e32 v238, v238, v238
	v_max_f32_e32 v239, v239, v239
	v_max_f32_e32 v240, v240, v240
	v_max_f32_e32 v241, v241, v241
	v_med3_f32 v226, v226, s62, v95
	v_med3_f32 v227, v227, s62, v95
	v_med3_f32 v228, v228, s62, v95
	v_med3_f32 v229, v229, s62, v95
	v_med3_f32 v230, v230, s62, v95
	v_med3_f32 v231, v231, s62, v95
	v_med3_f32 v232, v232, s62, v95
	v_med3_f32 v233, v233, s62, v95
	v_med3_f32 v234, v234, s62, v95
	v_med3_f32 v235, v235, s62, v95
	v_med3_f32 v236, v236, s62, v95
	v_med3_f32 v237, v237, s62, v95
	v_med3_f32 v238, v238, s62, v95
	v_med3_f32 v239, v239, s62, v95
	v_med3_f32 v240, v240, s62, v95
	v_med3_f32 v241, v241, s62, v95
	v_mov_b32_e32 v242, 0
	v_mov_b32_e32 v243, 0
	v_mov_b32_e32 v244, 0
	v_mov_b32_e32 v245, 0
	v_cvt_pk_fp8_f32 v242, v226, v227
	v_cvt_pk_fp8_f32 v243, v230, v231
	v_cvt_pk_fp8_f32 v244, v234, v235
	v_cvt_pk_fp8_f32 v245, v238, v239
	v_cvt_pk_fp8_f32 v242, v228, v229 op_sel:[0,0,1]
	v_cvt_pk_fp8_f32 v243, v232, v233 op_sel:[0,0,1]
	v_cvt_pk_fp8_f32 v244, v236, v237 op_sel:[0,0,1]
	v_cvt_pk_fp8_f32 v245, v240, v241 op_sel:[0,0,1]
	s_nop 0
	global_store_dwordx4 v78, v[242:245], s[6:7]
	s_waitcnt vmcnt(12)
	v_mul_f32_e32 v144, v34, v144
	v_mul_f32_e32 v145, v34, v145
	v_mul_f32_e32 v146, v34, v146
	v_mul_f32_e32 v147, v34, v147
	ds_write_b128 v209, v[144:147]
	v_mul_f32_e32 v148, v35, v148
	v_mul_f32_e32 v149, v35, v149
	v_mul_f32_e32 v150, v35, v150
	v_mul_f32_e32 v151, v35, v151
	ds_write_b128 v209, v[148:151] offset:1024
	v_mul_f32_e32 v152, v36, v152
	v_mul_f32_e32 v153, v36, v153
	v_mul_f32_e32 v154, v36, v154
	v_mul_f32_e32 v155, v36, v155
	ds_write_b128 v209, v[152:155] offset:2048
	v_mul_f32_e32 v156, v37, v156
	v_mul_f32_e32 v157, v37, v157
	v_mul_f32_e32 v158, v37, v158
	v_mul_f32_e32 v159, v37, v159
	ds_write_b128 v209, v[156:159] offset:3072
	v_mul_f32_e32 v160, v38, v160
	v_mul_f32_e32 v161, v38, v161
	v_mul_f32_e32 v162, v38, v162
	v_mul_f32_e32 v163, v38, v163
	ds_write_b128 v209, v[160:163] offset:4096
	v_mul_f32_e32 v164, v39, v164
	v_mul_f32_e32 v165, v39, v165
	v_mul_f32_e32 v166, v39, v166
	v_mul_f32_e32 v167, v39, v167
	ds_write_b128 v209, v[164:167] offset:5120
	v_mul_f32_e32 v168, v40, v168
	v_mul_f32_e32 v169, v40, v169
	v_mul_f32_e32 v170, v40, v170
	v_mul_f32_e32 v171, v40, v171
	ds_write_b128 v209, v[168:171] offset:6144
	v_mul_f32_e32 v172, v41, v172
	v_mul_f32_e32 v173, v41, v173
	v_mul_f32_e32 v174, v41, v174
	v_mul_f32_e32 v175, v41, v175
	ds_write_b128 v209, v[172:175] offset:7168
	s_waitcnt lgkmcnt(0)
	s_barrier
; #define GAS __attribute__((address_space(1)))
; #define LAS __attribute__((address_space(3)))
; #define LDS_WAIT() asm volatile("s_waitcnt lgkmcnt(0)" ::: "memory")
; __device__ __forceinline__ unsigned pk4_fp8(float a, float b, float c, float d) {
;     a = fminf(fmaxf(a, -448.f), 448.f); b = fminf(fmaxf(b, -448.f), 448.f); c = fminf(fmaxf(c, -448.f), 448.f); d = fminf(fmaxf(d, -448.f), 448.f);
;     int w = __builtin_amdgcn_cvt_pk_fp8_f32(a, b, 0, false); w = __builtin_amdgcn_cvt_pk_fp8_f32(c, d, w, true); return (unsigned)w; }
;     const int pr = item >> 1, kb = 2 * (pr / nblk) + (item & 1), nb = pr % nblk, k0 = 64 * kb, n0 = 32 * nb;
;     const int nr = n0 + (lane & 31); const int sc = MAP == 1 ? src_col_in(nr) : nr;
;     float v[32];
; #pragma unroll
;     for (int i = 0; i < 32; ++i) v[i] = sc >= 0 ? W[(size_t)(k0 + 2 * i + (lane >> 5)) * Nsrc + sc] : 0.f;
; #pragma unroll
;     for (int i = 0; i < 32; ++i) { const int k = k0 + 2 * i + (lane >> 5); float x = v[i] * wscale; if (KS) x *= (k < ksplit ? ksA[k] : ksB[k - ksplit]); scr[(2 * i + (lane >> 5)) * 33 + (lane & 31)] = x; }
;     LDS_WAIT(); asm volatile("" ::: "memory");
;     const int c = lane & 7;
; #pragma unroll
;     for (int j = 0; j < 4; ++j) { const int n = (lane >> 3) + 8 * j; const LAS float* s = scr + (8 * c) * 33 + n;
;         const unsigned long long o = (unsigned long long)pg8::pk4_fp8(s[0 * 33], s[1 * 33], s[2 * 33], s[3 * 33]) | ((unsigned long long)pg8::pk4_fp8(s[4 * 33], s[5 * 33], s[6 * 33], s[7 * 33]) << 32);
;         *(GAS unsigned long long*)(WT + (size_t)(n0 + n) * K + k0 + 8 * c) = o; }
;     LDS_WAIT(); asm volatile("" ::: "memory");
; }
	s_add_u32 s8, s34, 0x6000
	s_addc_u32 s9, s35, 0
	global_load_dwordx4 v[144:147], v74, s[8:9]
	s_add_u32 s8, s8, 0x20000
	s_addc_u32 s9, s9, 0
	global_load_dwordx4 v[148:151], v74, s[8:9]
	s_add_u32 s8, s8, 0x20000
	s_addc_u32 s9, s9, 0
	global_load_dwordx4 v[152:155], v74, s[8:9]
	s_add_u32 s8, s8, 0x20000
	s_addc_u32 s9, s9, 0
	global_load_dwordx4 v[156:159], v74, s[8:9]
	s_add_u32 s8, s8, 0x20000
	s_addc_u32 s9, s9, 0
	global_load_dwordx4 v[160:163], v74, s[8:9]
	s_add_u32 s8, s8, 0x20000
	s_addc_u32 s9, s9, 0
	global_load_dwordx4 v[164:167], v74, s[8:9]
	s_add_u32 s8, s8, 0x20000
	s_addc_u32 s9, s9, 0
	global_load_dwordx4 v[168:171], v74, s[8:9]
	s_add_u32 s8, s8, 0x20000
	s_addc_u32 s9, s9, 0
	global_load_dwordx4 v[172:175], v74, s[8:9]
	s_add_u32 s6, s36, 0x1000000
	s_addc_u32 s7, s37, 0
	ds_read_b32 v226, v211
	ds_read_b32 v227, v211 offset:512
	ds_read_b32 v228, v211 offset:1024
	ds_read_b32 v229, v211 offset:1536
	ds_read_b32 v230, v211 offset:2048
	ds_read_b32 v231, v211 offset:2560
	ds_read_b32 v232, v211 offset:3072
	ds_read_b32 v233, v211 offset:3584
	ds_read_b32 v234, v211 offset:4096
	ds_read_b32 v235, v211 offset:4608
	ds_read_b32 v236, v211 offset:5120
	ds_read_b32 v237, v211 offset:5632
	ds_read_b32 v238, v211 offset:6144
	ds_read_b32 v239, v211 offset:6656
	ds_read_b32 v240, v211 offset:7168
	ds_read_b32 v241, v211 offset:7680
	s_waitcnt lgkmcnt(0)
	v_max_f32_e32 v226, v226, v226
	v_max_f32_e32 v227, v227, v227
	v_max_f32_e32 v228, v228, v228
	v_max_f32_e32 v229, v229, v229
	v_max_f32_e32 v230, v230, v230
	v_max_f32_e32 v231, v231, v231
	v_max_f32_e32 v232, v232, v232
	v_max_f32_e32 v233, v233, v233
	v_max_f32_e32 v234, v234, v234
	v_max_f32_e32 v235, v235, v235
	v_max_f32_e32 v236, v236, v236
	v_max_f32_e32 v237, v237, v237
	v_max_f32_e32 v238, v238, v238
	v_max_f32_e32 v239, v239, v239
	v_max_f32_e32 v240, v240, v240
	v_max_f32_e32 v241, v241, v241
	v_med3_f32 v226, v226, s62, v95
	v_med3_f32 v227, v227, s62, v95
	v_med3_f32 v228, v228, s62, v95
	v_med3_f32 v229, v229, s62, v95
	v_med3_f32 v230, v230, s62, v95
	v_med3_f32 v231, v231, s62, v95
	v_med3_f32 v232, v232, s62, v95
	v_med3_f32 v233, v233, s62, v95
	v_med3_f32 v234, v234, s62, v95
	v_med3_f32 v235, v235, s62, v95
	v_med3_f32 v236, v236, s62, v95
	v_med3_f32 v237, v237, s62, v95
	v_med3_f32 v238, v238, s62, v95
	v_med3_f32 v239, v239, s62, v95
	v_med3_f32 v240, v240, s62, v95
	v_med3_f32 v241, v241, s62, v95
	v_mov_b32_e32 v242, 0
	v_mov_b32_e32 v243, 0
	v_mov_b32_e32 v244, 0
	v_mov_b32_e32 v245, 0
	v_cvt_pk_fp8_f32 v242, v226, v227
	v_cvt_pk_fp8_f32 v243, v230, v231
	v_cvt_pk_fp8_f32 v244, v234, v235
	v_cvt_pk_fp8_f32 v245, v238, v239
	v_cvt_pk_fp8_f32 v242, v228, v229 op_sel:[0,0,1]
	v_cvt_pk_fp8_f32 v243, v232, v233 op_sel:[0,0,1]
	v_cvt_pk_fp8_f32 v244, v236, v237 op_sel:[0,0,1]
	v_cvt_pk_fp8_f32 v245, v240, v241 op_sel:[0,0,1]
	s_nop 0
	global_store_dwordx4 v77, v[242:245], s[6:7]
	ds_read_b32 v226, v213
	ds_read_b32 v227, v213 offset:512
	ds_read_b32 v228, v213 offset:1024
	ds_read_b32 v229, v213 offset:1536
	ds_read_b32 v230, v213 offset:2048
	ds_read_b32 v231, v213 offset:2560
	ds_read_b32 v232, v213 offset:3072
	ds_read_b32 v233, v213 offset:3584
	ds_read_b32 v234, v213 offset:4096
	ds_read_b32 v235, v213 offset:4608
	ds_read_b32 v236, v213 offset:5120
	ds_read_b32 v237, v213 offset:5632
	ds_read_b32 v238, v213 offset:6144
	ds_read_b32 v239, v213 offset:6656
	ds_read_b32 v240, v213 offset:7168
	ds_read_b32 v241, v213 offset:7680
	s_waitcnt lgkmcnt(0)
	v_max_f32_e32 v226, v226, v226
	v_max_f32_e32 v227, v227, v227
	v_max_f32_e32 v228, v228, v228
	v_max_f32_e32 v229, v229, v229
	v_max_f32_e32 v230, v230, v230
	v_max_f32_e32 v231, v231, v231
	v_max_f32_e32 v232, v232, v232
	v_max_f32_e32 v233, v233, v233
	v_max_f32_e32 v234, v234, v234
	v_max_f32_e32 v235, v235, v235
	v_max_f32_e32 v236, v236, v236
	v_max_f32_e32 v237, v237, v237
	v_max_f32_e32 v238, v238, v238
	v_max_f32_e32 v239, v239, v239
	v_max_f32_e32 v240, v240, v240
	v_max_f32_e32 v241, v241, v241
	v_med3_f32 v226, v226, s62, v95
	v_med3_f32 v227, v227, s62, v95
	v_med3_f32 v228, v228, s62, v95
	v_med3_f32 v229, v229, s62, v95
	v_med3_f32 v230, v230, s62, v95
	v_med3_f32 v231, v231, s62, v95
	v_med3_f32 v232, v232, s62, v95
	v_med3_f32 v233, v233, s62, v95
	v_med3_f32 v234, v234, s62, v95
	v_med3_f32 v235, v235, s62, v95
	v_med3_f32 v236, v236, s62, v95
	v_med3_f32 v237, v237, s62, v95
	v_med3_f32 v238, v238, s62, v95
	v_med3_f32 v239, v239, s62, v95
	v_med3_f32 v240, v240, s62, v95
	v_med3_f32 v241, v241, s62, v95
	v_mov_b32_e32 v242, 0
	v_mov_b32_e32 v243, 0
	v_mov_b32_e32 v244, 0
	v_mov_b32_e32 v245, 0
	v_cvt_pk_fp8_f32 v242, v226, v227
	v_cvt_pk_fp8_f32 v243, v230, v231
	v_cvt_pk_fp8_f32 v244, v234, v235
	v_cvt_pk_fp8_f32 v245, v238, v239
	v_cvt_pk_fp8_f32 v242, v228, v229 op_sel:[0,0,1]
	v_cvt_pk_fp8_f32 v243, v232, v233 op_sel:[0,0,1]
	v_cvt_pk_fp8_f32 v244, v236, v237 op_sel:[0,0,1]
	v_cvt_pk_fp8_f32 v245, v240, v241 op_sel:[0,0,1]
	s_nop 0
	global_store_dwordx4 v78, v[242:245], s[6:7]
	s_waitcnt vmcnt(12)
	v_mul_f32_e32 v176, v34, v176
	v_mul_f32_e32 v177, v34, v177
	v_mul_f32_e32 v178, v34, v178
	v_mul_f32_e32 v179, v34, v179
	ds_write_b128 v210, v[176:179]
	v_mul_f32_e32 v180, v35, v180
	v_mul_f32_e32 v181, v35, v181
	v_mul_f32_e32 v182, v35, v182
	v_mul_f32_e32 v183, v35, v183
	ds_write_b128 v210, v[180:183] offset:1024
	v_mul_f32_e32 v184, v36, v184
	v_mul_f32_e32 v185, v36, v185
	v_mul_f32_e32 v186, v36, v186
	v_mul_f32_e32 v187, v36, v187
	ds_write_b128 v210, v[184:187] offset:2048
	v_mul_f32_e32 v188, v37, v188
	v_mul_f32_e32 v189, v37, v189
	v_mul_f32_e32 v190, v37, v190
	v_mul_f32_e32 v191, v37, v191
	ds_write_b128 v210, v[188:191] offset:3072
	v_mul_f32_e32 v192, v38, v192
	v_mul_f32_e32 v193, v38, v193
	v_mul_f32_e32 v194, v38, v194
	v_mul_f32_e32 v195, v38, v195
	ds_write_b128 v210, v[192:195] offset:4096
	v_mul_f32_e32 v196, v39, v196
	v_mul_f32_e32 v197, v39, v197
	v_mul_f32_e32 v198, v39, v198
	v_mul_f32_e32 v199, v39, v199
	ds_write_b128 v210, v[196:199] offset:5120
	v_mul_f32_e32 v200, v40, v200
	v_mul_f32_e32 v201, v40, v201
	v_mul_f32_e32 v202, v40, v202
	v_mul_f32_e32 v203, v40, v203
	ds_write_b128 v210, v[200:203] offset:6144
	v_mul_f32_e32 v204, v41, v204
	v_mul_f32_e32 v205, v41, v205
	v_mul_f32_e32 v206, v41, v206
	v_mul_f32_e32 v207, v41, v207
	ds_write_b128 v210, v[204:207] offset:7168
	s_waitcnt lgkmcnt(0)
	s_barrier
; #define GAS __attribute__((address_space(1)))
; #define LAS __attribute__((address_space(3)))
; #define LDS_WAIT() asm volatile("s_waitcnt lgkmcnt(0)" ::: "memory")
; __device__ __forceinline__ unsigned pk4_fp8(float a, float b, float c, float d) {
;     a = fminf(fmaxf(a, -448.f), 448.f); b = fminf(fmaxf(b, -448.f), 448.f); c = fminf(fmaxf(c, -448.f), 448.f); d = fminf(fmaxf(d, -448.f), 448.f);
;     int w = __builtin_amdgcn_cvt_pk_fp8_f32(a, b, 0, false); w = __builtin_amdgcn_cvt_pk_fp8_f32(c, d, w, true); return (unsigned)w; }
;     const int pr = item >> 1, kb = 2 * (pr / nblk) + (item & 1), nb = pr % nblk, k0 = 64 * kb, n0 = 32 * nb;
;     const int nr = n0 + (lane & 31); const int sc = MAP == 1 ? src_col_in(nr) : nr;
;     float v[32];
; #pragma unroll
;     for (int i = 0; i < 32; ++i) v[i] = sc >= 0 ? W[(size_t)(k0 + 2 * i + (lane >> 5)) * Nsrc + sc] : 0.f;
; #pragma unroll
;     for (int i = 0; i < 32; ++i) { const int k = k0 + 2 * i + (lane >> 5); float x = v[i] * wscale; if (KS) x *= (k < ksplit ? ksA[k] : ksB[k - ksplit]); scr[(2 * i + (lane >> 5)) * 33 + (lane & 31)] = x; }
;     LDS_WAIT(); asm volatile("" ::: "memory");
;     const int c = lane & 7;
; #pragma unroll
;     for (int j = 0; j < 4; ++j) { const int n = (lane >> 3) + 8 * j; const LAS float* s = scr + (8 * c) * 33 + n;
;         const unsigned long long o = (unsigned long long)pg8::pk4_fp8(s[0 * 33], s[1 * 33], s[2 * 33], s[3 * 33]) | ((unsigned long long)pg8::pk4_fp8(s[4 * 33], s[5 * 33], s[6 * 33], s[7 * 33]) << 32);
;         *(GAS unsigned long long*)(WT + (size_t)(n0 + n) * K + k0 + 8 * c) = o; }
;     LDS_WAIT(); asm volatile("" ::: "memory");
; }
	s_add_u32 s8, s34, 0x7000
	s_addc_u32 s9, s35, 0
	global_load_dwordx4 v[176:179], v74, s[8:9]
	s_add_u32 s8, s8, 0x20000
	s_addc_u32 s9, s9, 0
	global_load_dwordx4 v[180:183], v74, s[8:9]
	s_add_u32 s8, s8, 0x20000
	s_addc_u32 s9, s9, 0
	global_load_dwordx4 v[184:187], v74, s[8:9]
	s_add_u32 s8, s8, 0x20000
	s_addc_u32 s9, s9, 0
	global_load_dwordx4 v[188:191], v74, s[8:9]
	s_add_u32 s8, s8, 0x20000
	s_addc_u32 s9, s9, 0
	global_load_dwordx4 v[192:195], v74, s[8:9]
	s_add_u32 s8, s8, 0x20000
	s_addc_u32 s9, s9, 0
	global_load_dwordx4 v[196:199], v74, s[8:9]
	s_add_u32 s8, s8, 0x20000
	s_addc_u32 s9, s9, 0
	global_load_dwordx4 v[200:203], v74, s[8:9]
	s_add_u32 s8, s8, 0x20000
	s_addc_u32 s9, s9, 0
	global_load_dwordx4 v[204:207], v74, s[8:9]
	s_add_u32 s6, s36, 0x1400000
	s_addc_u32 s7, s37, 0
	ds_read_b32 v226, v212
	ds_read_b32 v227, v212 offset:512
	ds_read_b32 v228, v212 offset:1024
	ds_read_b32 v229, v212 offset:1536
	ds_read_b32 v230, v212 offset:2048
	ds_read_b32 v231, v212 offset:2560
	ds_read_b32 v232, v212 offset:3072
	ds_read_b32 v233, v212 offset:3584
	ds_read_b32 v234, v212 offset:4096
	ds_read_b32 v235, v212 offset:4608
	ds_read_b32 v236, v212 offset:5120
	ds_read_b32 v237, v212 offset:5632
	ds_read_b32 v238, v212 offset:6144
	ds_read_b32 v239, v212 offset:6656
	ds_read_b32 v240, v212 offset:7168
	ds_read_b32 v241, v212 offset:7680
	s_waitcnt lgkmcnt(0)
	v_max_f32_e32 v226, v226, v226
	v_max_f32_e32 v227, v227, v227
	v_max_f32_e32 v228, v228, v228
	v_max_f32_e32 v229, v229, v229
	v_max_f32_e32 v230, v230, v230
	v_max_f32_e32 v231, v231, v231
	v_max_f32_e32 v232, v232, v232
	v_max_f32_e32 v233, v233, v233
	v_max_f32_e32 v234, v234, v234
	v_max_f32_e32 v235, v235, v235
	v_max_f32_e32 v236, v236, v236
	v_max_f32_e32 v237, v237, v237
	v_max_f32_e32 v238, v238, v238
	v_max_f32_e32 v239, v239, v239
	v_max_f32_e32 v240, v240, v240
	v_max_f32_e32 v241, v241, v241
	v_med3_f32 v226, v226, s62, v95
	v_med3_f32 v227, v227, s62, v95
	v_med3_f32 v228, v228, s62, v95
	v_med3_f32 v229, v229, s62, v95
	v_med3_f32 v230, v230, s62, v95
	v_med3_f32 v231, v231, s62, v95
	v_med3_f32 v232, v232, s62, v95
	v_med3_f32 v233, v233, s62, v95
	v_med3_f32 v234, v234, s62, v95
	v_med3_f32 v235, v235, s62, v95
	v_med3_f32 v236, v236, s62, v95
	v_med3_f32 v237, v237, s62, v95
	v_med3_f32 v238, v238, s62, v95
	v_med3_f32 v239, v239, s62, v95
	v_med3_f32 v240, v240, s62, v95
	v_med3_f32 v241, v241, s62, v95
	v_mov_b32_e32 v242, 0
	v_mov_b32_e32 v243, 0
	v_mov_b32_e32 v244, 0
	v_mov_b32_e32 v245, 0
	v_cvt_pk_fp8_f32 v242, v226, v227
	v_cvt_pk_fp8_f32 v243, v230, v231
	v_cvt_pk_fp8_f32 v244, v234, v235
	v_cvt_pk_fp8_f32 v245, v238, v239
	v_cvt_pk_fp8_f32 v242, v228, v229 op_sel:[0,0,1]
	v_cvt_pk_fp8_f32 v243, v232, v233 op_sel:[0,0,1]
	v_cvt_pk_fp8_f32 v244, v236, v237 op_sel:[0,0,1]
	v_cvt_pk_fp8_f32 v245, v240, v241 op_sel:[0,0,1]
	s_nop 0
	global_store_dwordx4 v77, v[242:245], s[6:7]
	ds_read_b32 v226, v214
	ds_read_b32 v227, v214 offset:512
	ds_read_b32 v228, v214 offset:1024
	ds_read_b32 v229, v214 offset:1536
	ds_read_b32 v230, v214 offset:2048
	ds_read_b32 v231, v214 offset:2560
	ds_read_b32 v232, v214 offset:3072
	ds_read_b32 v233, v214 offset:3584
	ds_read_b32 v234, v214 offset:4096
	ds_read_b32 v235, v214 offset:4608
	ds_read_b32 v236, v214 offset:5120
	ds_read_b32 v237, v214 offset:5632
	ds_read_b32 v238, v214 offset:6144
	ds_read_b32 v239, v214 offset:6656
	ds_read_b32 v240, v214 offset:7168
	ds_read_b32 v241, v214 offset:7680
	s_waitcnt lgkmcnt(0)
	v_max_f32_e32 v226, v226, v226
	v_max_f32_e32 v227, v227, v227
	v_max_f32_e32 v228, v228, v228
	v_max_f32_e32 v229, v229, v229
	v_max_f32_e32 v230, v230, v230
	v_max_f32_e32 v231, v231, v231
	v_max_f32_e32 v232, v232, v232
	v_max_f32_e32 v233, v233, v233
	v_max_f32_e32 v234, v234, v234
	v_max_f32_e32 v235, v235, v235
	v_max_f32_e32 v236, v236, v236
	v_max_f32_e32 v237, v237, v237
	v_max_f32_e32 v238, v238, v238
	v_max_f32_e32 v239, v239, v239
	v_max_f32_e32 v240, v240, v240
	v_max_f32_e32 v241, v241, v241
	v_med3_f32 v226, v226, s62, v95
	v_med3_f32 v227, v227, s62, v95
	v_med3_f32 v228, v228, s62, v95
	v_med3_f32 v229, v229, s62, v95
	v_med3_f32 v230, v230, s62, v95
	v_med3_f32 v231, v231, s62, v95
	v_med3_f32 v232, v232, s62, v95
	v_med3_f32 v233, v233, s62, v95
	v_med3_f32 v234, v234, s62, v95
	v_med3_f32 v235, v235, s62, v95
	v_med3_f32 v236, v236, s62, v95
	v_med3_f32 v237, v237, s62, v95
	v_med3_f32 v238, v238, s62, v95
	v_med3_f32 v239, v239, s62, v95
	v_med3_f32 v240, v240, s62, v95
	v_med3_f32 v241, v241, s62, v95
	v_mov_b32_e32 v242, 0
	v_mov_b32_e32 v243, 0
	v_mov_b32_e32 v244, 0
	v_mov_b32_e32 v245, 0
	v_cvt_pk_fp8_f32 v242, v226, v227
	v_cvt_pk_fp8_f32 v243, v230, v231
	v_cvt_pk_fp8_f32 v244, v234, v235
	v_cvt_pk_fp8_f32 v245, v238, v239
	v_cvt_pk_fp8_f32 v242, v228, v229 op_sel:[0,0,1]
	v_cvt_pk_fp8_f32 v243, v232, v233 op_sel:[0,0,1]
	v_cvt_pk_fp8_f32 v244, v236, v237 op_sel:[0,0,1]
	v_cvt_pk_fp8_f32 v245, v240, v241 op_sel:[0,0,1]
	s_nop 0
	global_store_dwordx4 v78, v[242:245], s[6:7]
	s_waitcnt vmcnt(12)
	v_mul_f32_e32 v144, v34, v144
	v_mul_f32_e32 v145, v34, v145
	v_mul_f32_e32 v146, v34, v146
	v_mul_f32_e32 v147, v34, v147
	ds_write_b128 v209, v[144:147]
	v_mul_f32_e32 v148, v35, v148
	v_mul_f32_e32 v149, v35, v149
	v_mul_f32_e32 v150, v35, v150
	v_mul_f32_e32 v151, v35, v151
	ds_write_b128 v209, v[148:151] offset:1024
	v_mul_f32_e32 v152, v36, v152
	v_mul_f32_e32 v153, v36, v153
	v_mul_f32_e32 v154, v36, v154
	v_mul_f32_e32 v155, v36, v155
	ds_write_b128 v209, v[152:155] offset:2048
	v_mul_f32_e32 v156, v37, v156
	v_mul_f32_e32 v157, v37, v157
	v_mul_f32_e32 v158, v37, v158
	v_mul_f32_e32 v159, v37, v159
	ds_write_b128 v209, v[156:159] offset:3072
	v_mul_f32_e32 v160, v38, v160
	v_mul_f32_e32 v161, v38, v161
	v_mul_f32_e32 v162, v38, v162
	v_mul_f32_e32 v163, v38, v163
	ds_write_b128 v209, v[160:163] offset:4096
	v_mul_f32_e32 v164, v39, v164
	v_mul_f32_e32 v165, v39, v165
	v_mul_f32_e32 v166, v39, v166
	v_mul_f32_e32 v167, v39, v167
	ds_write_b128 v209, v[164:167] offset:5120
	v_mul_f32_e32 v168, v40, v168
	v_mul_f32_e32 v169, v40, v169
	v_mul_f32_e32 v170, v40, v170
	v_mul_f32_e32 v171, v40, v171
	ds_write_b128 v209, v[168:171] offset:6144
	v_mul_f32_e32 v172, v41, v172
	v_mul_f32_e32 v173, v41, v173
	v_mul_f32_e32 v174, v41, v174
	v_mul_f32_e32 v175, v41, v175
	ds_write_b128 v209, v[172:175] offset:7168
	s_waitcnt lgkmcnt(0)
	s_barrier
; #define GAS __attribute__((address_space(1)))
; #define LAS __attribute__((address_space(3)))
; #define LDS_WAIT() asm volatile("s_waitcnt lgkmcnt(0)" ::: "memory")
; __device__ __forceinline__ unsigned pk4_fp8(float a, float b, float c, float d) {
;     a = fminf(fmaxf(a, -448.f), 448.f); b = fminf(fmaxf(b, -448.f), 448.f); c = fminf(fmaxf(c, -448.f), 448.f); d = fminf(fmaxf(d, -448.f), 448.f);
;     int w = __builtin_amdgcn_cvt_pk_fp8_f32(a, b, 0, false); w = __builtin_amdgcn_cvt_pk_fp8_f32(c, d, w, true); return (unsigned)w; }
;     const int pr = item >> 1, kb = 2 * (pr / nblk) + (item & 1), nb = pr % nblk, k0 = 64 * kb, n0 = 32 * nb;
;     const int nr = n0 + (lane & 31); const int sc = MAP == 1 ? src_col_in(nr) : nr;
;     float v[32];
; #pragma unroll
;     for (int i = 0; i < 32; ++i) v[i] = sc >= 0 ? W[(size_t)(k0 + 2 * i + (lane >> 5)) * Nsrc + sc] : 0.f;
; #pragma unroll
;     for (int i = 0; i < 32; ++i) { const int k = k0 + 2 * i + (lane >> 5); float x = v[i] * wscale; if (KS) x *= (k < ksplit ? ksA[k] : ksB[k - ksplit]); scr[(2 * i + (lane >> 5)) * 33 + (lane & 31)] = x; }
;     LDS_WAIT(); asm volatile("" ::: "memory");
;     const int c = lane & 7;
; #pragma unroll
;     for (int j = 0; j < 4; ++j) { const int n = (lane >> 3) + 8 * j; const LAS float* s = scr + (8 * c) * 33 + n;
;         const unsigned long long o = (unsigned long long)pg8::pk4_fp8(s[0 * 33], s[1 * 33], s[2 * 33], s[3 * 33]) | ((unsigned long long)pg8::pk4_fp8(s[4 * 33], s[5 * 33], s[6 * 33], s[7 * 33]) << 32);
;         *(GAS unsigned long long*)(WT + (size_t)(n0 + n) * K + k0 + 8 * c) = o; }
;     LDS_WAIT(); asm volatile("" ::: "memory");
; }
	s_add_u32 s8, s34, 0x8000
	s_addc_u32 s9, s35, 0
	global_load_dwordx4 v[144:147], v74, s[8:9]
	s_add_u32 s8, s8, 0x20000
	s_addc_u32 s9, s9, 0
	global_load_dwordx4 v[148:151], v74, s[8:9]
	s_add_u32 s8, s8, 0x20000
	s_addc_u32 s9, s9, 0
	global_load_dwordx4 v[152:155], v74, s[8:9]
	s_add_u32 s8, s8, 0x20000
	s_addc_u32 s9, s9, 0
	global_load_dwordx4 v[156:159], v74, s[8:9]
	s_add_u32 s8, s8, 0x20000
	s_addc_u32 s9, s9, 0
	global_load_dwordx4 v[160:163], v74, s[8:9]
	s_add_u32 s8, s8, 0x20000
	s_addc_u32 s9, s9, 0
	global_load_dwordx4 v[164:167], v74, s[8:9]
	s_add_u32 s8, s8, 0x20000
	s_addc_u32 s9, s9, 0
	global_load_dwordx4 v[168:171], v74, s[8:9]
	s_add_u32 s8, s8, 0x20000
	s_addc_u32 s9, s9, 0
	global_load_dwordx4 v[172:175], v74, s[8:9]
	s_add_u32 s6, s36, 0x1800000
	s_addc_u32 s7, s37, 0
	ds_read_b32 v226, v211
	ds_read_b32 v227, v211 offset:512
	ds_read_b32 v228, v211 offset:1024
	ds_read_b32 v229, v211 offset:1536
	ds_read_b32 v230, v211 offset:2048
	ds_read_b32 v231, v211 offset:2560
	ds_read_b32 v232, v211 offset:3072
	ds_read_b32 v233, v211 offset:3584
	ds_read_b32 v234, v211 offset:4096
	ds_read_b32 v235, v211 offset:4608
	ds_read_b32 v236, v211 offset:5120
	ds_read_b32 v237, v211 offset:5632
	ds_read_b32 v238, v211 offset:6144
	ds_read_b32 v239, v211 offset:6656
	ds_read_b32 v240, v211 offset:7168
	ds_read_b32 v241, v211 offset:7680
	s_waitcnt lgkmcnt(0)
	v_max_f32_e32 v226, v226, v226
	v_max_f32_e32 v227, v227, v227
	v_max_f32_e32 v228, v228, v228
	v_max_f32_e32 v229, v229, v229
	v_max_f32_e32 v230, v230, v230
	v_max_f32_e32 v231, v231, v231
	v_max_f32_e32 v232, v232, v232
	v_max_f32_e32 v233, v233, v233
	v_max_f32_e32 v234, v234, v234
	v_max_f32_e32 v235, v235, v235
	v_max_f32_e32 v236, v236, v236
	v_max_f32_e32 v237, v237, v237
	v_max_f32_e32 v238, v238, v238
	v_max_f32_e32 v239, v239, v239
	v_max_f32_e32 v240, v240, v240
	v_max_f32_e32 v241, v241, v241
	v_med3_f32 v226, v226, s62, v95
	v_med3_f32 v227, v227, s62, v95
	v_med3_f32 v228, v228, s62, v95
	v_med3_f32 v229, v229, s62, v95
	v_med3_f32 v230, v230, s62, v95
	v_med3_f32 v231, v231, s62, v95
	v_med3_f32 v232, v232, s62, v95
	v_med3_f32 v233, v233, s62, v95
	v_med3_f32 v234, v234, s62, v95
	v_med3_f32 v235, v235, s62, v95
	v_med3_f32 v236, v236, s62, v95
	v_med3_f32 v237, v237, s62, v95
	v_med3_f32 v238, v238, s62, v95
	v_med3_f32 v239, v239, s62, v95
	v_med3_f32 v240, v240, s62, v95
	v_med3_f32 v241, v241, s62, v95
	v_mov_b32_e32 v242, 0
	v_mov_b32_e32 v243, 0
	v_mov_b32_e32 v244, 0
	v_mov_b32_e32 v245, 0
	v_cvt_pk_fp8_f32 v242, v226, v227
	v_cvt_pk_fp8_f32 v243, v230, v231
	v_cvt_pk_fp8_f32 v244, v234, v235
	v_cvt_pk_fp8_f32 v245, v238, v239
	v_cvt_pk_fp8_f32 v242, v228, v229 op_sel:[0,0,1]
	v_cvt_pk_fp8_f32 v243, v232, v233 op_sel:[0,0,1]
	v_cvt_pk_fp8_f32 v244, v236, v237 op_sel:[0,0,1]
	v_cvt_pk_fp8_f32 v245, v240, v241 op_sel:[0,0,1]
	s_nop 0
	global_store_dwordx4 v77, v[242:245], s[6:7]
	ds_read_b32 v226, v213
	ds_read_b32 v227, v213 offset:512
	ds_read_b32 v228, v213 offset:1024
	ds_read_b32 v229, v213 offset:1536
	ds_read_b32 v230, v213 offset:2048
	ds_read_b32 v231, v213 offset:2560
	ds_read_b32 v232, v213 offset:3072
	ds_read_b32 v233, v213 offset:3584
	ds_read_b32 v234, v213 offset:4096
	ds_read_b32 v235, v213 offset:4608
	ds_read_b32 v236, v213 offset:5120
	ds_read_b32 v237, v213 offset:5632
	ds_read_b32 v238, v213 offset:6144
	ds_read_b32 v239, v213 offset:6656
	ds_read_b32 v240, v213 offset:7168
	ds_read_b32 v241, v213 offset:7680
	s_waitcnt lgkmcnt(0)
	v_max_f32_e32 v226, v226, v226
	v_max_f32_e32 v227, v227, v227
	v_max_f32_e32 v228, v228, v228
	v_max_f32_e32 v229, v229, v229
	v_max_f32_e32 v230, v230, v230
	v_max_f32_e32 v231, v231, v231
	v_max_f32_e32 v232, v232, v232
	v_max_f32_e32 v233, v233, v233
	v_max_f32_e32 v234, v234, v234
	v_max_f32_e32 v235, v235, v235
	v_max_f32_e32 v236, v236, v236
	v_max_f32_e32 v237, v237, v237
	v_max_f32_e32 v238, v238, v238
	v_max_f32_e32 v239, v239, v239
	v_max_f32_e32 v240, v240, v240
	v_max_f32_e32 v241, v241, v241
	v_med3_f32 v226, v226, s62, v95
	v_med3_f32 v227, v227, s62, v95
	v_med3_f32 v228, v228, s62, v95
	v_med3_f32 v229, v229, s62, v95
	v_med3_f32 v230, v230, s62, v95
	v_med3_f32 v231, v231, s62, v95
	v_med3_f32 v232, v232, s62, v95
	v_med3_f32 v233, v233, s62, v95
	v_med3_f32 v234, v234, s62, v95
	v_med3_f32 v235, v235, s62, v95
	v_med3_f32 v236, v236, s62, v95
	v_med3_f32 v237, v237, s62, v95
	v_med3_f32 v238, v238, s62, v95
	v_med3_f32 v239, v239, s62, v95
	v_med3_f32 v240, v240, s62, v95
	v_med3_f32 v241, v241, s62, v95
	v_mov_b32_e32 v242, 0
	v_mov_b32_e32 v243, 0
	v_mov_b32_e32 v244, 0
	v_mov_b32_e32 v245, 0
	v_cvt_pk_fp8_f32 v242, v226, v227
	v_cvt_pk_fp8_f32 v243, v230, v231
	v_cvt_pk_fp8_f32 v244, v234, v235
	v_cvt_pk_fp8_f32 v245, v238, v239
	v_cvt_pk_fp8_f32 v242, v228, v229 op_sel:[0,0,1]
	v_cvt_pk_fp8_f32 v243, v232, v233 op_sel:[0,0,1]
	v_cvt_pk_fp8_f32 v244, v236, v237 op_sel:[0,0,1]
	v_cvt_pk_fp8_f32 v245, v240, v241 op_sel:[0,0,1]
	s_nop 0
	global_store_dwordx4 v78, v[242:245], s[6:7]
	s_waitcnt vmcnt(12)
	v_mul_f32_e32 v176, v34, v176
	v_mul_f32_e32 v177, v34, v177
	v_mul_f32_e32 v178, v34, v178
	v_mul_f32_e32 v179, v34, v179
	ds_write_b128 v210, v[176:179]
	v_mul_f32_e32 v180, v35, v180
	v_mul_f32_e32 v181, v35, v181
	v_mul_f32_e32 v182, v35, v182
	v_mul_f32_e32 v183, v35, v183
	ds_write_b128 v210, v[180:183] offset:1024
	v_mul_f32_e32 v184, v36, v184
	v_mul_f32_e32 v185, v36, v185
	v_mul_f32_e32 v186, v36, v186
	v_mul_f32_e32 v187, v36, v187
	ds_write_b128 v210, v[184:187] offset:2048
	v_mul_f32_e32 v188, v37, v188
	v_mul_f32_e32 v189, v37, v189
	v_mul_f32_e32 v190, v37, v190
	v_mul_f32_e32 v191, v37, v191
	ds_write_b128 v210, v[188:191] offset:3072
	v_mul_f32_e32 v192, v38, v192
	v_mul_f32_e32 v193, v38, v193
	v_mul_f32_e32 v194, v38, v194
	v_mul_f32_e32 v195, v38, v195
	ds_write_b128 v210, v[192:195] offset:4096
	v_mul_f32_e32 v196, v39, v196
	v_mul_f32_e32 v197, v39, v197
	v_mul_f32_e32 v198, v39, v198
	v_mul_f32_e32 v199, v39, v199
	ds_write_b128 v210, v[196:199] offset:5120
	v_mul_f32_e32 v200, v40, v200
	v_mul_f32_e32 v201, v40, v201
	v_mul_f32_e32 v202, v40, v202
	v_mul_f32_e32 v203, v40, v203
	ds_write_b128 v210, v[200:203] offset:6144
	v_mul_f32_e32 v204, v41, v204
	v_mul_f32_e32 v205, v41, v205
	v_mul_f32_e32 v206, v41, v206
	v_mul_f32_e32 v207, v41, v207
	ds_write_b128 v210, v[204:207] offset:7168
	s_waitcnt lgkmcnt(0)
	s_barrier
; #define GAS __attribute__((address_space(1)))
; #define LAS __attribute__((address_space(3)))
; #define LDS_WAIT() asm volatile("s_waitcnt lgkmcnt(0)" ::: "memory")
; __device__ __forceinline__ unsigned pk4_fp8(float a, float b, float c, float d) {
;     a = fminf(fmaxf(a, -448.f), 448.f); b = fminf(fmaxf(b, -448.f), 448.f); c = fminf(fmaxf(c, -448.f), 448.f); d = fminf(fmaxf(d, -448.f), 448.f);
;     int w = __builtin_amdgcn_cvt_pk_fp8_f32(a, b, 0, false); w = __builtin_amdgcn_cvt_pk_fp8_f32(c, d, w, true); return (unsigned)w; }
;     const int pr = item >> 1, kb = 2 * (pr / nblk) + (item & 1), nb = pr % nblk, k0 = 64 * kb, n0 = 32 * nb;
;     const int nr = n0 + (lane & 31); const int sc = MAP == 1 ? src_col_in(nr) : nr;
;     float v[32];
; #pragma unroll
;     for (int i = 0; i < 32; ++i) v[i] = sc >= 0 ? W[(size_t)(k0 + 2 * i + (lane >> 5)) * Nsrc + sc] : 0.f;
; #pragma unroll
;     for (int i = 0; i < 32; ++i) { const int k = k0 + 2 * i + (lane >> 5); float x = v[i] * wscale; if (KS) x *= (k < ksplit ? ksA[k] : ksB[k - ksplit]); scr[(2 * i + (lane >> 5)) * 33 + (lane & 31)] = x; }
;     LDS_WAIT(); asm volatile("" ::: "memory");
;     const int c = lane & 7;
; #pragma unroll
;     for (int j = 0; j < 4; ++j) { const int n = (lane >> 3) + 8 * j; const LAS float* s = scr + (8 * c) * 33 + n;
;         const unsigned long long o = (unsigned long long)pg8::pk4_fp8(s[0 * 33], s[1 * 33], s[2 * 33], s[3 * 33]) | ((unsigned long long)pg8::pk4_fp8(s[4 * 33], s[5 * 33], s[6 * 33], s[7 * 33]) << 32);
;         *(GAS unsigned long long*)(WT + (size_t)(n0 + n) * K + k0 + 8 * c) = o; }
;     LDS_WAIT(); asm volatile("" ::: "memory");
; }
	s_add_u32 s8, s34, 0x9000
	s_addc_u32 s9, s35, 0
	global_load_dwordx4 v[176:179], v74, s[8:9]
	s_add_u32 s8, s8, 0x20000
	s_addc_u32 s9, s9, 0
	global_load_dwordx4 v[180:183], v74, s[8:9]
	s_add_u32 s8, s8, 0x20000
	s_addc_u32 s9, s9, 0
	global_load_dwordx4 v[184:187], v74, s[8:9]
	s_add_u32 s8, s8, 0x20000
	s_addc_u32 s9, s9, 0
	global_load_dwordx4 v[188:191], v74, s[8:9]
	s_add_u32 s8, s8, 0x20000
	s_addc_u32 s9, s9, 0
	global_load_dwordx4 v[192:195], v74, s[8:9]
	s_add_u32 s8, s8, 0x20000
	s_addc_u32 s9, s9, 0
	global_load_dwordx4 v[196:199], v74, s[8:9]
	s_add_u32 s8, s8, 0x20000
	s_addc_u32 s9, s9, 0
	global_load_dwordx4 v[200:203], v74, s[8:9]
	s_add_u32 s8, s8, 0x20000
	s_addc_u32 s9, s9, 0
	global_load_dwordx4 v[204:207], v74, s[8:9]
	s_add_u32 s6, s36, 0x1c00000
	s_addc_u32 s7, s37, 0
	ds_read_b32 v226, v212
	ds_read_b32 v227, v212 offset:512
	ds_read_b32 v228, v212 offset:1024
	ds_read_b32 v229, v212 offset:1536
	ds_read_b32 v230, v212 offset:2048
	ds_read_b32 v231, v212 offset:2560
	ds_read_b32 v232, v212 offset:3072
	ds_read_b32 v233, v212 offset:3584
	ds_read_b32 v234, v212 offset:4096
	ds_read_b32 v235, v212 offset:4608
	ds_read_b32 v236, v212 offset:5120
	ds_read_b32 v237, v212 offset:5632
	ds_read_b32 v238, v212 offset:6144
	ds_read_b32 v239, v212 offset:6656
	ds_read_b32 v240, v212 offset:7168
	ds_read_b32 v241, v212 offset:7680
	s_waitcnt lgkmcnt(0)
	v_max_f32_e32 v226, v226, v226
	v_max_f32_e32 v227, v227, v227
	v_max_f32_e32 v228, v228, v228
	v_max_f32_e32 v229, v229, v229
	v_max_f32_e32 v230, v230, v230
	v_max_f32_e32 v231, v231, v231
	v_max_f32_e32 v232, v232, v232
	v_max_f32_e32 v233, v233, v233
	v_max_f32_e32 v234, v234, v234
	v_max_f32_e32 v235, v235, v235
	v_max_f32_e32 v236, v236, v236
	v_max_f32_e32 v237, v237, v237
	v_max_f32_e32 v238, v238, v238
	v_max_f32_e32 v239, v239, v239
	v_max_f32_e32 v240, v240, v240
	v_max_f32_e32 v241, v241, v241
	v_med3_f32 v226, v226, s62, v95
	v_med3_f32 v227, v227, s62, v95
	v_med3_f32 v228, v228, s62, v95
	v_med3_f32 v229, v229, s62, v95
	v_med3_f32 v230, v230, s62, v95
	v_med3_f32 v231, v231, s62, v95
	v_med3_f32 v232, v232, s62, v95
	v_med3_f32 v233, v233, s62, v95
	v_med3_f32 v234, v234, s62, v95
	v_med3_f32 v235, v235, s62, v95
	v_med3_f32 v236, v236, s62, v95
	v_med3_f32 v237, v237, s62, v95
	v_med3_f32 v238, v238, s62, v95
	v_med3_f32 v239, v239, s62, v95
	v_med3_f32 v240, v240, s62, v95
	v_med3_f32 v241, v241, s62, v95
	v_mov_b32_e32 v242, 0
	v_mov_b32_e32 v243, 0
	v_mov_b32_e32 v244, 0
	v_mov_b32_e32 v245, 0
	v_cvt_pk_fp8_f32 v242, v226, v227
	v_cvt_pk_fp8_f32 v243, v230, v231
	v_cvt_pk_fp8_f32 v244, v234, v235
	v_cvt_pk_fp8_f32 v245, v238, v239
	v_cvt_pk_fp8_f32 v242, v228, v229 op_sel:[0,0,1]
	v_cvt_pk_fp8_f32 v243, v232, v233 op_sel:[0,0,1]
	v_cvt_pk_fp8_f32 v244, v236, v237 op_sel:[0,0,1]
	v_cvt_pk_fp8_f32 v245, v240, v241 op_sel:[0,0,1]
	s_nop 0
	global_store_dwordx4 v77, v[242:245], s[6:7]
	ds_read_b32 v226, v214
	ds_read_b32 v227, v214 offset:512
	ds_read_b32 v228, v214 offset:1024
	ds_read_b32 v229, v214 offset:1536
	ds_read_b32 v230, v214 offset:2048
	ds_read_b32 v231, v214 offset:2560
	ds_read_b32 v232, v214 offset:3072
	ds_read_b32 v233, v214 offset:3584
	ds_read_b32 v234, v214 offset:4096
	ds_read_b32 v235, v214 offset:4608
	ds_read_b32 v236, v214 offset:5120
	ds_read_b32 v237, v214 offset:5632
	ds_read_b32 v238, v214 offset:6144
	ds_read_b32 v239, v214 offset:6656
	ds_read_b32 v240, v214 offset:7168
	ds_read_b32 v241, v214 offset:7680
	s_waitcnt lgkmcnt(0)
	v_max_f32_e32 v226, v226, v226
	v_max_f32_e32 v227, v227, v227
	v_max_f32_e32 v228, v228, v228
	v_max_f32_e32 v229, v229, v229
	v_max_f32_e32 v230, v230, v230
	v_max_f32_e32 v231, v231, v231
	v_max_f32_e32 v232, v232, v232
	v_max_f32_e32 v233, v233, v233
	v_max_f32_e32 v234, v234, v234
	v_max_f32_e32 v235, v235, v235
	v_max_f32_e32 v236, v236, v236
	v_max_f32_e32 v237, v237, v237
	v_max_f32_e32 v238, v238, v238
	v_max_f32_e32 v239, v239, v239
	v_max_f32_e32 v240, v240, v240
	v_max_f32_e32 v241, v241, v241
	v_med3_f32 v226, v226, s62, v95
	v_med3_f32 v227, v227, s62, v95
	v_med3_f32 v228, v228, s62, v95
	v_med3_f32 v229, v229, s62, v95
	v_med3_f32 v230, v230, s62, v95
	v_med3_f32 v231, v231, s62, v95
	v_med3_f32 v232, v232, s62, v95
	v_med3_f32 v233, v233, s62, v95
	v_med3_f32 v234, v234, s62, v95
	v_med3_f32 v235, v235, s62, v95
	v_med3_f32 v236, v236, s62, v95
	v_med3_f32 v237, v237, s62, v95
	v_med3_f32 v238, v238, s62, v95
	v_med3_f32 v239, v239, s62, v95
	v_med3_f32 v240, v240, s62, v95
	v_med3_f32 v241, v241, s62, v95
	v_mov_b32_e32 v242, 0
	v_mov_b32_e32 v243, 0
	v_mov_b32_e32 v244, 0
	v_mov_b32_e32 v245, 0
	v_cvt_pk_fp8_f32 v242, v226, v227
	v_cvt_pk_fp8_f32 v243, v230, v231
	v_cvt_pk_fp8_f32 v244, v234, v235
	v_cvt_pk_fp8_f32 v245, v238, v239
	v_cvt_pk_fp8_f32 v242, v228, v229 op_sel:[0,0,1]
	v_cvt_pk_fp8_f32 v243, v232, v233 op_sel:[0,0,1]
	v_cvt_pk_fp8_f32 v244, v236, v237 op_sel:[0,0,1]
	v_cvt_pk_fp8_f32 v245, v240, v241 op_sel:[0,0,1]
	s_nop 0
	global_store_dwordx4 v78, v[242:245], s[6:7]
	s_waitcnt vmcnt(12)
	v_mul_f32_e32 v144, v34, v144
	v_mul_f32_e32 v145, v34, v145
	v_mul_f32_e32 v146, v34, v146
	v_mul_f32_e32 v147, v34, v147
	ds_write_b128 v209, v[144:147]
	v_mul_f32_e32 v148, v35, v148
	v_mul_f32_e32 v149, v35, v149
	v_mul_f32_e32 v150, v35, v150
	v_mul_f32_e32 v151, v35, v151
	ds_write_b128 v209, v[148:151] offset:1024
	v_mul_f32_e32 v152, v36, v152
	v_mul_f32_e32 v153, v36, v153
	v_mul_f32_e32 v154, v36, v154
	v_mul_f32_e32 v155, v36, v155
	ds_write_b128 v209, v[152:155] offset:2048
	v_mul_f32_e32 v156, v37, v156
	v_mul_f32_e32 v157, v37, v157
	v_mul_f32_e32 v158, v37, v158
	v_mul_f32_e32 v159, v37, v159
	ds_write_b128 v209, v[156:159] offset:3072
	v_mul_f32_e32 v160, v38, v160
	v_mul_f32_e32 v161, v38, v161
	v_mul_f32_e32 v162, v38, v162
	v_mul_f32_e32 v163, v38, v163
	ds_write_b128 v209, v[160:163] offset:4096
	v_mul_f32_e32 v164, v39, v164
	v_mul_f32_e32 v165, v39, v165
	v_mul_f32_e32 v166, v39, v166
	v_mul_f32_e32 v167, v39, v167
	ds_write_b128 v209, v[164:167] offset:5120
	v_mul_f32_e32 v168, v40, v168
	v_mul_f32_e32 v169, v40, v169
	v_mul_f32_e32 v170, v40, v170
	v_mul_f32_e32 v171, v40, v171
	ds_write_b128 v209, v[168:171] offset:6144
	v_mul_f32_e32 v172, v41, v172
	v_mul_f32_e32 v173, v41, v173
	v_mul_f32_e32 v174, v41, v174
	v_mul_f32_e32 v175, v41, v175
	ds_write_b128 v209, v[172:175] offset:7168
	s_waitcnt lgkmcnt(0)
	s_barrier
; #define GAS __attribute__((address_space(1)))
; #define LAS __attribute__((address_space(3)))
; #define LDS_WAIT() asm volatile("s_waitcnt lgkmcnt(0)" ::: "memory")
; __device__ __forceinline__ unsigned pk4_fp8(float a, float b, float c, float d) {
;     a = fminf(fmaxf(a, -448.f), 448.f); b = fminf(fmaxf(b, -448.f), 448.f); c = fminf(fmaxf(c, -448.f), 448.f); d = fminf(fmaxf(d, -448.f), 448.f);
;     int w = __builtin_amdgcn_cvt_pk_fp8_f32(a, b, 0, false); w = __builtin_amdgcn_cvt_pk_fp8_f32(c, d, w, true); return (unsigned)w; }
;     const int pr = item >> 1, kb = 2 * (pr / nblk) + (item & 1), nb = pr % nblk, k0 = 64 * kb, n0 = 32 * nb;
;     const int nr = n0 + (lane & 31); const int sc = MAP == 1 ? src_col_in(nr) : nr;
;     float v[32];
; #pragma unroll
;     for (int i = 0; i < 32; ++i) v[i] = sc >= 0 ? W[(size_t)(k0 + 2 * i + (lane >> 5)) * Nsrc + sc] : 0.f;
; #pragma unroll
;     for (int i = 0; i < 32; ++i) { const int k = k0 + 2 * i + (lane >> 5); float x = v[i] * wscale; if (KS) x *= (k < ksplit ? ksA[k] : ksB[k - ksplit]); scr[(2 * i + (lane >> 5)) * 33 + (lane & 31)] = x; }
;     LDS_WAIT(); asm volatile("" ::: "memory");
;     const int c = lane & 7;
; #pragma unroll
;     for (int j = 0; j < 4; ++j) { const int n = (lane >> 3) + 8 * j; const LAS float* s = scr + (8 * c) * 33 + n;
;         const unsigned long long o = (unsigned long long)pg8::pk4_fp8(s[0 * 33], s[1 * 33], s[2 * 33], s[3 * 33]) | ((unsigned long long)pg8::pk4_fp8(s[4 * 33], s[5 * 33], s[6 * 33], s[7 * 33]) << 32);
;         *(GAS unsigned long long*)(WT + (size_t)(n0 + n) * K + k0 + 8 * c) = o; }
;     LDS_WAIT(); asm volatile("" ::: "memory");
; }
	s_add_u32 s8, s34, 0xa000
	s_addc_u32 s9, s35, 0
	global_load_dwordx4 v[144:147], v74, s[8:9]
	s_add_u32 s8, s8, 0x20000
	s_addc_u32 s9, s9, 0
	global_load_dwordx4 v[148:151], v74, s[8:9]
	s_add_u32 s8, s8, 0x20000
	s_addc_u32 s9, s9, 0
	global_load_dwordx4 v[152:155], v74, s[8:9]
	s_add_u32 s8, s8, 0x20000
	s_addc_u32 s9, s9, 0
	global_load_dwordx4 v[156:159], v74, s[8:9]
	s_add_u32 s8, s8, 0x20000
	s_addc_u32 s9, s9, 0
	global_load_dwordx4 v[160:163], v74, s[8:9]
	s_add_u32 s8, s8, 0x20000
	s_addc_u32 s9, s9, 0
	global_load_dwordx4 v[164:167], v74, s[8:9]
	s_add_u32 s8, s8, 0x20000
	s_addc_u32 s9, s9, 0
	global_load_dwordx4 v[168:171], v74, s[8:9]
	s_add_u32 s8, s8, 0x20000
	s_addc_u32 s9, s9, 0
	global_load_dwordx4 v[172:175], v74, s[8:9]
	s_add_u32 s6, s36, 0x2000000
	s_addc_u32 s7, s37, 0
	ds_read_b32 v226, v211
	ds_read_b32 v227, v211 offset:512
	ds_read_b32 v228, v211 offset:1024
	ds_read_b32 v229, v211 offset:1536
	ds_read_b32 v230, v211 offset:2048
	ds_read_b32 v231, v211 offset:2560
	ds_read_b32 v232, v211 offset:3072
	ds_read_b32 v233, v211 offset:3584
	ds_read_b32 v234, v211 offset:4096
	ds_read_b32 v235, v211 offset:4608
	ds_read_b32 v236, v211 offset:5120
	ds_read_b32 v237, v211 offset:5632
	ds_read_b32 v238, v211 offset:6144
	ds_read_b32 v239, v211 offset:6656
	ds_read_b32 v240, v211 offset:7168
	ds_read_b32 v241, v211 offset:7680
	s_waitcnt lgkmcnt(0)
	v_max_f32_e32 v226, v226, v226
	v_max_f32_e32 v227, v227, v227
	v_max_f32_e32 v228, v228, v228
	v_max_f32_e32 v229, v229, v229
	v_max_f32_e32 v230, v230, v230
	v_max_f32_e32 v231, v231, v231
	v_max_f32_e32 v232, v232, v232
	v_max_f32_e32 v233, v233, v233
	v_max_f32_e32 v234, v234, v234
	v_max_f32_e32 v235, v235, v235
	v_max_f32_e32 v236, v236, v236
	v_max_f32_e32 v237, v237, v237
	v_max_f32_e32 v238, v238, v238
	v_max_f32_e32 v239, v239, v239
	v_max_f32_e32 v240, v240, v240
	v_max_f32_e32 v241, v241, v241
	v_med3_f32 v226, v226, s62, v95
	v_med3_f32 v227, v227, s62, v95
	v_med3_f32 v228, v228, s62, v95
	v_med3_f32 v229, v229, s62, v95
	v_med3_f32 v230, v230, s62, v95
	v_med3_f32 v231, v231, s62, v95
	v_med3_f32 v232, v232, s62, v95
	v_med3_f32 v233, v233, s62, v95
	v_med3_f32 v234, v234, s62, v95
	v_med3_f32 v235, v235, s62, v95
	v_med3_f32 v236, v236, s62, v95
	v_med3_f32 v237, v237, s62, v95
	v_med3_f32 v238, v238, s62, v95
	v_med3_f32 v239, v239, s62, v95
	v_med3_f32 v240, v240, s62, v95
	v_med3_f32 v241, v241, s62, v95
	v_mov_b32_e32 v242, 0
	v_mov_b32_e32 v243, 0
	v_mov_b32_e32 v244, 0
	v_mov_b32_e32 v245, 0
	v_cvt_pk_fp8_f32 v242, v226, v227
	v_cvt_pk_fp8_f32 v243, v230, v231
	v_cvt_pk_fp8_f32 v244, v234, v235
	v_cvt_pk_fp8_f32 v245, v238, v239
	v_cvt_pk_fp8_f32 v242, v228, v229 op_sel:[0,0,1]
	v_cvt_pk_fp8_f32 v243, v232, v233 op_sel:[0,0,1]
	v_cvt_pk_fp8_f32 v244, v236, v237 op_sel:[0,0,1]
	v_cvt_pk_fp8_f32 v245, v240, v241 op_sel:[0,0,1]
	s_nop 0
	global_store_dwordx4 v77, v[242:245], s[6:7]
	ds_read_b32 v226, v213
	ds_read_b32 v227, v213 offset:512
	ds_read_b32 v228, v213 offset:1024
	ds_read_b32 v229, v213 offset:1536
	ds_read_b32 v230, v213 offset:2048
	ds_read_b32 v231, v213 offset:2560
	ds_read_b32 v232, v213 offset:3072
	ds_read_b32 v233, v213 offset:3584
	ds_read_b32 v234, v213 offset:4096
	ds_read_b32 v235, v213 offset:4608
	ds_read_b32 v236, v213 offset:5120
	ds_read_b32 v237, v213 offset:5632
	ds_read_b32 v238, v213 offset:6144
	ds_read_b32 v239, v213 offset:6656
	ds_read_b32 v240, v213 offset:7168
	ds_read_b32 v241, v213 offset:7680
	s_waitcnt lgkmcnt(0)
	v_max_f32_e32 v226, v226, v226
	v_max_f32_e32 v227, v227, v227
	v_max_f32_e32 v228, v228, v228
	v_max_f32_e32 v229, v229, v229
	v_max_f32_e32 v230, v230, v230
	v_max_f32_e32 v231, v231, v231
	v_max_f32_e32 v232, v232, v232
	v_max_f32_e32 v233, v233, v233
	v_max_f32_e32 v234, v234, v234
	v_max_f32_e32 v235, v235, v235
	v_max_f32_e32 v236, v236, v236
	v_max_f32_e32 v237, v237, v237
	v_max_f32_e32 v238, v238, v238
	v_max_f32_e32 v239, v239, v239
	v_max_f32_e32 v240, v240, v240
	v_max_f32_e32 v241, v241, v241
	v_med3_f32 v226, v226, s62, v95
	v_med3_f32 v227, v227, s62, v95
	v_med3_f32 v228, v228, s62, v95
	v_med3_f32 v229, v229, s62, v95
	v_med3_f32 v230, v230, s62, v95
	v_med3_f32 v231, v231, s62, v95
	v_med3_f32 v232, v232, s62, v95
	v_med3_f32 v233, v233, s62, v95
	v_med3_f32 v234, v234, s62, v95
	v_med3_f32 v235, v235, s62, v95
	v_med3_f32 v236, v236, s62, v95
	v_med3_f32 v237, v237, s62, v95
	v_med3_f32 v238, v238, s62, v95
	v_med3_f32 v239, v239, s62, v95
	v_med3_f32 v240, v240, s62, v95
	v_med3_f32 v241, v241, s62, v95
	v_mov_b32_e32 v242, 0
	v_mov_b32_e32 v243, 0
	v_mov_b32_e32 v244, 0
	v_mov_b32_e32 v245, 0
	v_cvt_pk_fp8_f32 v242, v226, v227
	v_cvt_pk_fp8_f32 v243, v230, v231
	v_cvt_pk_fp8_f32 v244, v234, v235
	v_cvt_pk_fp8_f32 v245, v238, v239
	v_cvt_pk_fp8_f32 v242, v228, v229 op_sel:[0,0,1]
	v_cvt_pk_fp8_f32 v243, v232, v233 op_sel:[0,0,1]
	v_cvt_pk_fp8_f32 v244, v236, v237 op_sel:[0,0,1]
	v_cvt_pk_fp8_f32 v245, v240, v241 op_sel:[0,0,1]
	s_nop 0
	global_store_dwordx4 v78, v[242:245], s[6:7]
	s_waitcnt vmcnt(12)
	v_mul_f32_e32 v176, v34, v176
	v_mul_f32_e32 v177, v34, v177
	v_mul_f32_e32 v178, v34, v178
	v_mul_f32_e32 v179, v34, v179
	ds_write_b128 v210, v[176:179]
	v_mul_f32_e32 v180, v35, v180
	v_mul_f32_e32 v181, v35, v181
	v_mul_f32_e32 v182, v35, v182
	v_mul_f32_e32 v183, v35, v183
	ds_write_b128 v210, v[180:183] offset:1024
	v_mul_f32_e32 v184, v36, v184
	v_mul_f32_e32 v185, v36, v185
	v_mul_f32_e32 v186, v36, v186
	v_mul_f32_e32 v187, v36, v187
	ds_write_b128 v210, v[184:187] offset:2048
	v_mul_f32_e32 v188, v37, v188
	v_mul_f32_e32 v189, v37, v189
	v_mul_f32_e32 v190, v37, v190
	v_mul_f32_e32 v191, v37, v191
	ds_write_b128 v210, v[188:191] offset:3072
	v_mul_f32_e32 v192, v38, v192
	v_mul_f32_e32 v193, v38, v193
	v_mul_f32_e32 v194, v38, v194
	v_mul_f32_e32 v195, v38, v195
	ds_write_b128 v210, v[192:195] offset:4096
	v_mul_f32_e32 v196, v39, v196
	v_mul_f32_e32 v197, v39, v197
	v_mul_f32_e32 v198, v39, v198
	v_mul_f32_e32 v199, v39, v199
	ds_write_b128 v210, v[196:199] offset:5120
	v_mul_f32_e32 v200, v40, v200
	v_mul_f32_e32 v201, v40, v201
	v_mul_f32_e32 v202, v40, v202
	v_mul_f32_e32 v203, v40, v203
	ds_write_b128 v210, v[200:203] offset:6144
	v_mul_f32_e32 v204, v41, v204
	v_mul_f32_e32 v205, v41, v205
	v_mul_f32_e32 v206, v41, v206
	v_mul_f32_e32 v207, v41, v207
	ds_write_b128 v210, v[204:207] offset:7168
	s_waitcnt lgkmcnt(0)
	s_barrier
; #define GAS __attribute__((address_space(1)))
; #define LAS __attribute__((address_space(3)))
; #define LDS_WAIT() asm volatile("s_waitcnt lgkmcnt(0)" ::: "memory")
; __device__ __forceinline__ unsigned pk4_fp8(float a, float b, float c, float d) {
;     a = fminf(fmaxf(a, -448.f), 448.f); b = fminf(fmaxf(b, -448.f), 448.f); c = fminf(fmaxf(c, -448.f), 448.f); d = fminf(fmaxf(d, -448.f), 448.f);
;     int w = __builtin_amdgcn_cvt_pk_fp8_f32(a, b, 0, false); w = __builtin_amdgcn_cvt_pk_fp8_f32(c, d, w, true); return (unsigned)w; }
;     const int pr = item >> 1, kb = 2 * (pr / nblk) + (item & 1), nb = pr % nblk, k0 = 64 * kb, n0 = 32 * nb;
;     const int nr = n0 + (lane & 31); const int sc = MAP == 1 ? src_col_in(nr) : nr;
;     float v[32];
; #pragma unroll
;     for (int i = 0; i < 32; ++i) v[i] = sc >= 0 ? W[(size_t)(k0 + 2 * i + (lane >> 5)) * Nsrc + sc] : 0.f;
; #pragma unroll
;     for (int i = 0; i < 32; ++i) { const int k = k0 + 2 * i + (lane >> 5); float x = v[i] * wscale; if (KS) x *= (k < ksplit ? ksA[k] : ksB[k - ksplit]); scr[(2 * i + (lane >> 5)) * 33 + (lane & 31)] = x; }
;     LDS_WAIT(); asm volatile("" ::: "memory");
;     const int c = lane & 7;
; #pragma unroll
;     for (int j = 0; j < 4; ++j) { const int n = (lane >> 3) + 8 * j; const LAS float* s = scr + (8 * c) * 33 + n;
;         const unsigned long long o = (unsigned long long)pg8::pk4_fp8(s[0 * 33], s[1 * 33], s[2 * 33], s[3 * 33]) | ((unsigned long long)pg8::pk4_fp8(s[4 * 33], s[5 * 33], s[6 * 33], s[7 * 33]) << 32);
;         *(GAS unsigned long long*)(WT + (size_t)(n0 + n) * K + k0 + 8 * c) = o; }
;     LDS_WAIT(); asm volatile("" ::: "memory");
; }
	s_add_u32 s8, s34, 0xb000
	s_addc_u32 s9, s35, 0
	global_load_dwordx4 v[176:179], v74, s[8:9]
	s_add_u32 s8, s8, 0x20000
	s_addc_u32 s9, s9, 0
	global_load_dwordx4 v[180:183], v74, s[8:9]
	s_add_u32 s8, s8, 0x20000
	s_addc_u32 s9, s9, 0
	global_load_dwordx4 v[184:187], v74, s[8:9]
	s_add_u32 s8, s8, 0x20000
	s_addc_u32 s9, s9, 0
	global_load_dwordx4 v[188:191], v74, s[8:9]
	s_add_u32 s8, s8, 0x20000
	s_addc_u32 s9, s9, 0
	global_load_dwordx4 v[192:195], v74, s[8:9]
	s_add_u32 s8, s8, 0x20000
	s_addc_u32 s9, s9, 0
	global_load_dwordx4 v[196:199], v74, s[8:9]
	s_add_u32 s8, s8, 0x20000
	s_addc_u32 s9, s9, 0
	global_load_dwordx4 v[200:203], v74, s[8:9]
	s_add_u32 s8, s8, 0x20000
	s_addc_u32 s9, s9, 0
	global_load_dwordx4 v[204:207], v74, s[8:9]
	s_add_u32 s6, s36, 0x2400000
	s_addc_u32 s7, s37, 0
	ds_read_b32 v226, v212
	ds_read_b32 v227, v212 offset:512
	ds_read_b32 v228, v212 offset:1024
	ds_read_b32 v229, v212 offset:1536
	ds_read_b32 v230, v212 offset:2048
	ds_read_b32 v231, v212 offset:2560
	ds_read_b32 v232, v212 offset:3072
	ds_read_b32 v233, v212 offset:3584
	ds_read_b32 v234, v212 offset:4096
	ds_read_b32 v235, v212 offset:4608
	ds_read_b32 v236, v212 offset:5120
	ds_read_b32 v237, v212 offset:5632
	ds_read_b32 v238, v212 offset:6144
	ds_read_b32 v239, v212 offset:6656
	ds_read_b32 v240, v212 offset:7168
	ds_read_b32 v241, v212 offset:7680
	s_waitcnt lgkmcnt(0)
	v_max_f32_e32 v226, v226, v226
	v_max_f32_e32 v227, v227, v227
	v_max_f32_e32 v228, v228, v228
	v_max_f32_e32 v229, v229, v229
	v_max_f32_e32 v230, v230, v230
	v_max_f32_e32 v231, v231, v231
	v_max_f32_e32 v232, v232, v232
	v_max_f32_e32 v233, v233, v233
	v_max_f32_e32 v234, v234, v234
	v_max_f32_e32 v235, v235, v235
	v_max_f32_e32 v236, v236, v236
	v_max_f32_e32 v237, v237, v237
	v_max_f32_e32 v238, v238, v238
	v_max_f32_e32 v239, v239, v239
	v_max_f32_e32 v240, v240, v240
	v_max_f32_e32 v241, v241, v241
	v_med3_f32 v226, v226, s62, v95
	v_med3_f32 v227, v227, s62, v95
	v_med3_f32 v228, v228, s62, v95
	v_med3_f32 v229, v229, s62, v95
	v_med3_f32 v230, v230, s62, v95
	v_med3_f32 v231, v231, s62, v95
	v_med3_f32 v232, v232, s62, v95
	v_med3_f32 v233, v233, s62, v95
	v_med3_f32 v234, v234, s62, v95
	v_med3_f32 v235, v235, s62, v95
	v_med3_f32 v236, v236, s62, v95
	v_med3_f32 v237, v237, s62, v95
	v_med3_f32 v238, v238, s62, v95
	v_med3_f32 v239, v239, s62, v95
	v_med3_f32 v240, v240, s62, v95
	v_med3_f32 v241, v241, s62, v95
	v_mov_b32_e32 v242, 0
	v_mov_b32_e32 v243, 0
	v_mov_b32_e32 v244, 0
	v_mov_b32_e32 v245, 0
	v_cvt_pk_fp8_f32 v242, v226, v227
	v_cvt_pk_fp8_f32 v243, v230, v231
	v_cvt_pk_fp8_f32 v244, v234, v235
	v_cvt_pk_fp8_f32 v245, v238, v239
	v_cvt_pk_fp8_f32 v242, v228, v229 op_sel:[0,0,1]
	v_cvt_pk_fp8_f32 v243, v232, v233 op_sel:[0,0,1]
	v_cvt_pk_fp8_f32 v244, v236, v237 op_sel:[0,0,1]
	v_cvt_pk_fp8_f32 v245, v240, v241 op_sel:[0,0,1]
	s_nop 0
	global_store_dwordx4 v77, v[242:245], s[6:7]
	ds_read_b32 v226, v214
	ds_read_b32 v227, v214 offset:512
	ds_read_b32 v228, v214 offset:1024
	ds_read_b32 v229, v214 offset:1536
	ds_read_b32 v230, v214 offset:2048
	ds_read_b32 v231, v214 offset:2560
	ds_read_b32 v232, v214 offset:3072
	ds_read_b32 v233, v214 offset:3584
	ds_read_b32 v234, v214 offset:4096
	ds_read_b32 v235, v214 offset:4608
	ds_read_b32 v236, v214 offset:5120
	ds_read_b32 v237, v214 offset:5632
	ds_read_b32 v238, v214 offset:6144
	ds_read_b32 v239, v214 offset:6656
	ds_read_b32 v240, v214 offset:7168
	ds_read_b32 v241, v214 offset:7680
	s_waitcnt lgkmcnt(0)
	v_max_f32_e32 v226, v226, v226
	v_max_f32_e32 v227, v227, v227
	v_max_f32_e32 v228, v228, v228
	v_max_f32_e32 v229, v229, v229
	v_max_f32_e32 v230, v230, v230
	v_max_f32_e32 v231, v231, v231
	v_max_f32_e32 v232, v232, v232
	v_max_f32_e32 v233, v233, v233
	v_max_f32_e32 v234, v234, v234
	v_max_f32_e32 v235, v235, v235
	v_max_f32_e32 v236, v236, v236
	v_max_f32_e32 v237, v237, v237
	v_max_f32_e32 v238, v238, v238
	v_max_f32_e32 v239, v239, v239
	v_max_f32_e32 v240, v240, v240
	v_max_f32_e32 v241, v241, v241
	v_med3_f32 v226, v226, s62, v95
	v_med3_f32 v227, v227, s62, v95
	v_med3_f32 v228, v228, s62, v95
	v_med3_f32 v229, v229, s62, v95
	v_med3_f32 v230, v230, s62, v95
	v_med3_f32 v231, v231, s62, v95
	v_med3_f32 v232, v232, s62, v95
	v_med3_f32 v233, v233, s62, v95
	v_med3_f32 v234, v234, s62, v95
	v_med3_f32 v235, v235, s62, v95
	v_med3_f32 v236, v236, s62, v95
	v_med3_f32 v237, v237, s62, v95
	v_med3_f32 v238, v238, s62, v95
	v_med3_f32 v239, v239, s62, v95
	v_med3_f32 v240, v240, s62, v95
	v_med3_f32 v241, v241, s62, v95
	v_mov_b32_e32 v242, 0
	v_mov_b32_e32 v243, 0
	v_mov_b32_e32 v244, 0
	v_mov_b32_e32 v245, 0
	v_cvt_pk_fp8_f32 v242, v226, v227
	v_cvt_pk_fp8_f32 v243, v230, v231
	v_cvt_pk_fp8_f32 v244, v234, v235
	v_cvt_pk_fp8_f32 v245, v238, v239
	v_cvt_pk_fp8_f32 v242, v228, v229 op_sel:[0,0,1]
	v_cvt_pk_fp8_f32 v243, v232, v233 op_sel:[0,0,1]
	v_cvt_pk_fp8_f32 v244, v236, v237 op_sel:[0,0,1]
	v_cvt_pk_fp8_f32 v245, v240, v241 op_sel:[0,0,1]
	s_nop 0
	global_store_dwordx4 v78, v[242:245], s[6:7]
	s_waitcnt vmcnt(12)
	v_mul_f32_e32 v144, v34, v144
	v_mul_f32_e32 v145, v34, v145
	v_mul_f32_e32 v146, v34, v146
	v_mul_f32_e32 v147, v34, v147
	ds_write_b128 v209, v[144:147]
	v_mul_f32_e32 v148, v35, v148
	v_mul_f32_e32 v149, v35, v149
	v_mul_f32_e32 v150, v35, v150
	v_mul_f32_e32 v151, v35, v151
	ds_write_b128 v209, v[148:151] offset:1024
	v_mul_f32_e32 v152, v36, v152
	v_mul_f32_e32 v153, v36, v153
	v_mul_f32_e32 v154, v36, v154
	v_mul_f32_e32 v155, v36, v155
	ds_write_b128 v209, v[152:155] offset:2048
	v_mul_f32_e32 v156, v37, v156
	v_mul_f32_e32 v157, v37, v157
	v_mul_f32_e32 v158, v37, v158
	v_mul_f32_e32 v159, v37, v159
	ds_write_b128 v209, v[156:159] offset:3072
	v_mul_f32_e32 v160, v38, v160
	v_mul_f32_e32 v161, v38, v161
	v_mul_f32_e32 v162, v38, v162
	v_mul_f32_e32 v163, v38, v163
	ds_write_b128 v209, v[160:163] offset:4096
	v_mul_f32_e32 v164, v39, v164
	v_mul_f32_e32 v165, v39, v165
	v_mul_f32_e32 v166, v39, v166
	v_mul_f32_e32 v167, v39, v167
	ds_write_b128 v209, v[164:167] offset:5120
	v_mul_f32_e32 v168, v40, v168
	v_mul_f32_e32 v169, v40, v169
	v_mul_f32_e32 v170, v40, v170
	v_mul_f32_e32 v171, v40, v171
	ds_write_b128 v209, v[168:171] offset:6144
	v_mul_f32_e32 v172, v41, v172
	v_mul_f32_e32 v173, v41, v173
	v_mul_f32_e32 v174, v41, v174
	v_mul_f32_e32 v175, v41, v175
	ds_write_b128 v209, v[172:175] offset:7168
	s_waitcnt lgkmcnt(0)
	s_barrier
; #define GAS __attribute__((address_space(1)))
; #define LAS __attribute__((address_space(3)))
; #define LDS_WAIT() asm volatile("s_waitcnt lgkmcnt(0)" ::: "memory")
; __device__ __forceinline__ unsigned pk4_fp8(float a, float b, float c, float d) {
;     a = fminf(fmaxf(a, -448.f), 448.f); b = fminf(fmaxf(b, -448.f), 448.f); c = fminf(fmaxf(c, -448.f), 448.f); d = fminf(fmaxf(d, -448.f), 448.f);
;     int w = __builtin_amdgcn_cvt_pk_fp8_f32(a, b, 0, false); w = __builtin_amdgcn_cvt_pk_fp8_f32(c, d, w, true); return (unsigned)w; }
;     const int pr = item >> 1, kb = 2 * (pr / nblk) + (item & 1), nb = pr % nblk, k0 = 64 * kb, n0 = 32 * nb;
;     const int nr = n0 + (lane & 31); const int sc = MAP == 1 ? src_col_in(nr) : nr;
;     float v[32];
; #pragma unroll
;     for (int i = 0; i < 32; ++i) v[i] = sc >= 0 ? W[(size_t)(k0 + 2 * i + (lane >> 5)) * Nsrc + sc] : 0.f;
; #pragma unroll
;     for (int i = 0; i < 32; ++i) { const int k = k0 + 2 * i + (lane >> 5); float x = v[i] * wscale; if (KS) x *= (k < ksplit ? ksA[k] : ksB[k - ksplit]); scr[(2 * i + (lane >> 5)) * 33 + (lane & 31)] = x; }
;     LDS_WAIT(); asm volatile("" ::: "memory");
;     const int c = lane & 7;
; #pragma unroll
;     for (int j = 0; j < 4; ++j) { const int n = (lane >> 3) + 8 * j; const LAS float* s = scr + (8 * c) * 33 + n;
;         const unsigned long long o = (unsigned long long)pg8::pk4_fp8(s[0 * 33], s[1 * 33], s[2 * 33], s[3 * 33]) | ((unsigned long long)pg8::pk4_fp8(s[4 * 33], s[5 * 33], s[6 * 33], s[7 * 33]) << 32);
;         *(GAS unsigned long long*)(WT + (size_t)(n0 + n) * K + k0 + 8 * c) = o; }
;     LDS_WAIT(); asm volatile("" ::: "memory");
; }
	s_add_u32 s8, s34, 0xc000
	s_addc_u32 s9, s35, 0
	global_load_dwordx4 v[144:147], v74, s[8:9]
	s_add_u32 s8, s8, 0x20000
	s_addc_u32 s9, s9, 0
	global_load_dwordx4 v[148:151], v74, s[8:9]
	s_add_u32 s8, s8, 0x20000
	s_addc_u32 s9, s9, 0
	global_load_dwordx4 v[152:155], v74, s[8:9]
	s_add_u32 s8, s8, 0x20000
	s_addc_u32 s9, s9, 0
	global_load_dwordx4 v[156:159], v74, s[8:9]
	s_add_u32 s8, s8, 0x20000
	s_addc_u32 s9, s9, 0
	global_load_dwordx4 v[160:163], v74, s[8:9]
	s_add_u32 s8, s8, 0x20000
	s_addc_u32 s9, s9, 0
	global_load_dwordx4 v[164:167], v74, s[8:9]
	s_add_u32 s8, s8, 0x20000
	s_addc_u32 s9, s9, 0
	global_load_dwordx4 v[168:171], v74, s[8:9]
	s_add_u32 s8, s8, 0x20000
	s_addc_u32 s9, s9, 0
	global_load_dwordx4 v[172:175], v74, s[8:9]
	s_add_u32 s6, s36, 0x2800000
	s_addc_u32 s7, s37, 0
	ds_read_b32 v226, v211
	ds_read_b32 v227, v211 offset:512
	ds_read_b32 v228, v211 offset:1024
	ds_read_b32 v229, v211 offset:1536
	ds_read_b32 v230, v211 offset:2048
	ds_read_b32 v231, v211 offset:2560
	ds_read_b32 v232, v211 offset:3072
	ds_read_b32 v233, v211 offset:3584
	ds_read_b32 v234, v211 offset:4096
	ds_read_b32 v235, v211 offset:4608
	ds_read_b32 v236, v211 offset:5120
	ds_read_b32 v237, v211 offset:5632
	ds_read_b32 v238, v211 offset:6144
	ds_read_b32 v239, v211 offset:6656
	ds_read_b32 v240, v211 offset:7168
	ds_read_b32 v241, v211 offset:7680
	s_waitcnt lgkmcnt(0)
	v_max_f32_e32 v226, v226, v226
	v_max_f32_e32 v227, v227, v227
	v_max_f32_e32 v228, v228, v228
	v_max_f32_e32 v229, v229, v229
	v_max_f32_e32 v230, v230, v230
	v_max_f32_e32 v231, v231, v231
	v_max_f32_e32 v232, v232, v232
	v_max_f32_e32 v233, v233, v233
	v_max_f32_e32 v234, v234, v234
	v_max_f32_e32 v235, v235, v235
	v_max_f32_e32 v236, v236, v236
	v_max_f32_e32 v237, v237, v237
	v_max_f32_e32 v238, v238, v238
	v_max_f32_e32 v239, v239, v239
	v_max_f32_e32 v240, v240, v240
	v_max_f32_e32 v241, v241, v241
	v_med3_f32 v226, v226, s62, v95
	v_med3_f32 v227, v227, s62, v95
	v_med3_f32 v228, v228, s62, v95
	v_med3_f32 v229, v229, s62, v95
	v_med3_f32 v230, v230, s62, v95
	v_med3_f32 v231, v231, s62, v95
	v_med3_f32 v232, v232, s62, v95
	v_med3_f32 v233, v233, s62, v95
	v_med3_f32 v234, v234, s62, v95
	v_med3_f32 v235, v235, s62, v95
	v_med3_f32 v236, v236, s62, v95
	v_med3_f32 v237, v237, s62, v95
	v_med3_f32 v238, v238, s62, v95
	v_med3_f32 v239, v239, s62, v95
	v_med3_f32 v240, v240, s62, v95
	v_med3_f32 v241, v241, s62, v95
	v_mov_b32_e32 v242, 0
	v_mov_b32_e32 v243, 0
	v_mov_b32_e32 v244, 0
	v_mov_b32_e32 v245, 0
	v_cvt_pk_fp8_f32 v242, v226, v227
	v_cvt_pk_fp8_f32 v243, v230, v231
	v_cvt_pk_fp8_f32 v244, v234, v235
	v_cvt_pk_fp8_f32 v245, v238, v239
	v_cvt_pk_fp8_f32 v242, v228, v229 op_sel:[0,0,1]
	v_cvt_pk_fp8_f32 v243, v232, v233 op_sel:[0,0,1]
	v_cvt_pk_fp8_f32 v244, v236, v237 op_sel:[0,0,1]
	v_cvt_pk_fp8_f32 v245, v240, v241 op_sel:[0,0,1]
	s_nop 0
	global_store_dwordx4 v77, v[242:245], s[6:7]
	ds_read_b32 v226, v213
	ds_read_b32 v227, v213 offset:512
	ds_read_b32 v228, v213 offset:1024
	ds_read_b32 v229, v213 offset:1536
	ds_read_b32 v230, v213 offset:2048
	ds_read_b32 v231, v213 offset:2560
	ds_read_b32 v232, v213 offset:3072
	ds_read_b32 v233, v213 offset:3584
	ds_read_b32 v234, v213 offset:4096
	ds_read_b32 v235, v213 offset:4608
	ds_read_b32 v236, v213 offset:5120
	ds_read_b32 v237, v213 offset:5632
	ds_read_b32 v238, v213 offset:6144
	ds_read_b32 v239, v213 offset:6656
	ds_read_b32 v240, v213 offset:7168
	ds_read_b32 v241, v213 offset:7680
	s_waitcnt lgkmcnt(0)
	v_max_f32_e32 v226, v226, v226
	v_max_f32_e32 v227, v227, v227
	v_max_f32_e32 v228, v228, v228
	v_max_f32_e32 v229, v229, v229
	v_max_f32_e32 v230, v230, v230
	v_max_f32_e32 v231, v231, v231
	v_max_f32_e32 v232, v232, v232
	v_max_f32_e32 v233, v233, v233
	v_max_f32_e32 v234, v234, v234
	v_max_f32_e32 v235, v235, v235
	v_max_f32_e32 v236, v236, v236
	v_max_f32_e32 v237, v237, v237
	v_max_f32_e32 v238, v238, v238
	v_max_f32_e32 v239, v239, v239
	v_max_f32_e32 v240, v240, v240
	v_max_f32_e32 v241, v241, v241
	v_med3_f32 v226, v226, s62, v95
	v_med3_f32 v227, v227, s62, v95
	v_med3_f32 v228, v228, s62, v95
	v_med3_f32 v229, v229, s62, v95
	v_med3_f32 v230, v230, s62, v95
	v_med3_f32 v231, v231, s62, v95
	v_med3_f32 v232, v232, s62, v95
	v_med3_f32 v233, v233, s62, v95
	v_med3_f32 v234, v234, s62, v95
	v_med3_f32 v235, v235, s62, v95
	v_med3_f32 v236, v236, s62, v95
	v_med3_f32 v237, v237, s62, v95
	v_med3_f32 v238, v238, s62, v95
	v_med3_f32 v239, v239, s62, v95
	v_med3_f32 v240, v240, s62, v95
	v_med3_f32 v241, v241, s62, v95
	v_mov_b32_e32 v242, 0
	v_mov_b32_e32 v243, 0
	v_mov_b32_e32 v244, 0
	v_mov_b32_e32 v245, 0
	v_cvt_pk_fp8_f32 v242, v226, v227
	v_cvt_pk_fp8_f32 v243, v230, v231
	v_cvt_pk_fp8_f32 v244, v234, v235
	v_cvt_pk_fp8_f32 v245, v238, v239
	v_cvt_pk_fp8_f32 v242, v228, v229 op_sel:[0,0,1]
	v_cvt_pk_fp8_f32 v243, v232, v233 op_sel:[0,0,1]
	v_cvt_pk_fp8_f32 v244, v236, v237 op_sel:[0,0,1]
	v_cvt_pk_fp8_f32 v245, v240, v241 op_sel:[0,0,1]
	s_nop 0
	global_store_dwordx4 v78, v[242:245], s[6:7]
	s_waitcnt vmcnt(12)
	v_mul_f32_e32 v176, v34, v176
	v_mul_f32_e32 v177, v34, v177
	v_mul_f32_e32 v178, v34, v178
	v_mul_f32_e32 v179, v34, v179
	ds_write_b128 v210, v[176:179]
	v_mul_f32_e32 v180, v35, v180
	v_mul_f32_e32 v181, v35, v181
	v_mul_f32_e32 v182, v35, v182
	v_mul_f32_e32 v183, v35, v183
	ds_write_b128 v210, v[180:183] offset:1024
	v_mul_f32_e32 v184, v36, v184
	v_mul_f32_e32 v185, v36, v185
	v_mul_f32_e32 v186, v36, v186
	v_mul_f32_e32 v187, v36, v187
	ds_write_b128 v210, v[184:187] offset:2048
	v_mul_f32_e32 v188, v37, v188
	v_mul_f32_e32 v189, v37, v189
	v_mul_f32_e32 v190, v37, v190
	v_mul_f32_e32 v191, v37, v191
	ds_write_b128 v210, v[188:191] offset:3072
	v_mul_f32_e32 v192, v38, v192
	v_mul_f32_e32 v193, v38, v193
	v_mul_f32_e32 v194, v38, v194
	v_mul_f32_e32 v195, v38, v195
	ds_write_b128 v210, v[192:195] offset:4096
	v_mul_f32_e32 v196, v39, v196
	v_mul_f32_e32 v197, v39, v197
	v_mul_f32_e32 v198, v39, v198
	v_mul_f32_e32 v199, v39, v199
	ds_write_b128 v210, v[196:199] offset:5120
	v_mul_f32_e32 v200, v40, v200
	v_mul_f32_e32 v201, v40, v201
	v_mul_f32_e32 v202, v40, v202
	v_mul_f32_e32 v203, v40, v203
	ds_write_b128 v210, v[200:203] offset:6144
	v_mul_f32_e32 v204, v41, v204
	v_mul_f32_e32 v205, v41, v205
	v_mul_f32_e32 v206, v41, v206
	v_mul_f32_e32 v207, v41, v207
	ds_write_b128 v210, v[204:207] offset:7168
	s_waitcnt lgkmcnt(0)
	s_barrier
; #define GAS __attribute__((address_space(1)))
; #define LAS __attribute__((address_space(3)))
; #define LDS_WAIT() asm volatile("s_waitcnt lgkmcnt(0)" ::: "memory")
; __device__ __forceinline__ unsigned pk4_fp8(float a, float b, float c, float d) {
;     a = fminf(fmaxf(a, -448.f), 448.f); b = fminf(fmaxf(b, -448.f), 448.f); c = fminf(fmaxf(c, -448.f), 448.f); d = fminf(fmaxf(d, -448.f), 448.f);
;     int w = __builtin_amdgcn_cvt_pk_fp8_f32(a, b, 0, false); w = __builtin_amdgcn_cvt_pk_fp8_f32(c, d, w, true); return (unsigned)w; }
;     const int pr = item >> 1, kb = 2 * (pr / nblk) + (item & 1), nb = pr % nblk, k0 = 64 * kb, n0 = 32 * nb;
;     const int nr = n0 + (lane & 31); const int sc = MAP == 1 ? src_col_in(nr) : nr;
;     float v[32];
; #pragma unroll
;     for (int i = 0; i < 32; ++i) v[i] = sc >= 0 ? W[(size_t)(k0 + 2 * i + (lane >> 5)) * Nsrc + sc] : 0.f;
; #pragma unroll
;     for (int i = 0; i < 32; ++i) { const int k = k0 + 2 * i + (lane >> 5); float x = v[i] * wscale; if (KS) x *= (k < ksplit ? ksA[k] : ksB[k - ksplit]); scr[(2 * i + (lane >> 5)) * 33 + (lane & 31)] = x; }
;     LDS_WAIT(); asm volatile("" ::: "memory");
;     const int c = lane & 7;
; #pragma unroll
;     for (int j = 0; j < 4; ++j) { const int n = (lane >> 3) + 8 * j; const LAS float* s = scr + (8 * c) * 33 + n;
;         const unsigned long long o = (unsigned long long)pg8::pk4_fp8(s[0 * 33], s[1 * 33], s[2 * 33], s[3 * 33]) | ((unsigned long long)pg8::pk4_fp8(s[4 * 33], s[5 * 33], s[6 * 33], s[7 * 33]) << 32);
;         *(GAS unsigned long long*)(WT + (size_t)(n0 + n) * K + k0 + 8 * c) = o; }
;     LDS_WAIT(); asm volatile("" ::: "memory");
; }
	s_add_u32 s8, s34, 0xd000
	s_addc_u32 s9, s35, 0
	global_load_dwordx4 v[176:179], v74, s[8:9]
	s_add_u32 s8, s8, 0x20000
	s_addc_u32 s9, s9, 0
	global_load_dwordx4 v[180:183], v74, s[8:9]
	s_add_u32 s8, s8, 0x20000
	s_addc_u32 s9, s9, 0
	global_load_dwordx4 v[184:187], v74, s[8:9]
	s_add_u32 s8, s8, 0x20000
	s_addc_u32 s9, s9, 0
	global_load_dwordx4 v[188:191], v74, s[8:9]
	s_add_u32 s8, s8, 0x20000
	s_addc_u32 s9, s9, 0
	global_load_dwordx4 v[192:195], v74, s[8:9]
	s_add_u32 s8, s8, 0x20000
	s_addc_u32 s9, s9, 0
	global_load_dwordx4 v[196:199], v74, s[8:9]
	s_add_u32 s8, s8, 0x20000
	s_addc_u32 s9, s9, 0
	global_load_dwordx4 v[200:203], v74, s[8:9]
	s_add_u32 s8, s8, 0x20000
	s_addc_u32 s9, s9, 0
	global_load_dwordx4 v[204:207], v74, s[8:9]
	s_add_u32 s6, s36, 0x2c00000
	s_addc_u32 s7, s37, 0
	ds_read_b32 v226, v212
	ds_read_b32 v227, v212 offset:512
	ds_read_b32 v228, v212 offset:1024
	ds_read_b32 v229, v212 offset:1536
	ds_read_b32 v230, v212 offset:2048
	ds_read_b32 v231, v212 offset:2560
	ds_read_b32 v232, v212 offset:3072
	ds_read_b32 v233, v212 offset:3584
	ds_read_b32 v234, v212 offset:4096
	ds_read_b32 v235, v212 offset:4608
	ds_read_b32 v236, v212 offset:5120
	ds_read_b32 v237, v212 offset:5632
	ds_read_b32 v238, v212 offset:6144
	ds_read_b32 v239, v212 offset:6656
	ds_read_b32 v240, v212 offset:7168
	ds_read_b32 v241, v212 offset:7680
	s_waitcnt lgkmcnt(0)
	v_max_f32_e32 v226, v226, v226
	v_max_f32_e32 v227, v227, v227
	v_max_f32_e32 v228, v228, v228
	v_max_f32_e32 v229, v229, v229
	v_max_f32_e32 v230, v230, v230
	v_max_f32_e32 v231, v231, v231
	v_max_f32_e32 v232, v232, v232
	v_max_f32_e32 v233, v233, v233
	v_max_f32_e32 v234, v234, v234
	v_max_f32_e32 v235, v235, v235
	v_max_f32_e32 v236, v236, v236
	v_max_f32_e32 v237, v237, v237
	v_max_f32_e32 v238, v238, v238
	v_max_f32_e32 v239, v239, v239
	v_max_f32_e32 v240, v240, v240
	v_max_f32_e32 v241, v241, v241
	v_med3_f32 v226, v226, s62, v95
	v_med3_f32 v227, v227, s62, v95
	v_med3_f32 v228, v228, s62, v95
	v_med3_f32 v229, v229, s62, v95
	v_med3_f32 v230, v230, s62, v95
	v_med3_f32 v231, v231, s62, v95
	v_med3_f32 v232, v232, s62, v95
	v_med3_f32 v233, v233, s62, v95
	v_med3_f32 v234, v234, s62, v95
	v_med3_f32 v235, v235, s62, v95
	v_med3_f32 v236, v236, s62, v95
	v_med3_f32 v237, v237, s62, v95
	v_med3_f32 v238, v238, s62, v95
	v_med3_f32 v239, v239, s62, v95
	v_med3_f32 v240, v240, s62, v95
	v_med3_f32 v241, v241, s62, v95
	v_mov_b32_e32 v242, 0
	v_mov_b32_e32 v243, 0
	v_mov_b32_e32 v244, 0
	v_mov_b32_e32 v245, 0
	v_cvt_pk_fp8_f32 v242, v226, v227
	v_cvt_pk_fp8_f32 v243, v230, v231
	v_cvt_pk_fp8_f32 v244, v234, v235
	v_cvt_pk_fp8_f32 v245, v238, v239
	v_cvt_pk_fp8_f32 v242, v228, v229 op_sel:[0,0,1]
	v_cvt_pk_fp8_f32 v243, v232, v233 op_sel:[0,0,1]
	v_cvt_pk_fp8_f32 v244, v236, v237 op_sel:[0,0,1]
	v_cvt_pk_fp8_f32 v245, v240, v241 op_sel:[0,0,1]
	s_nop 0
	global_store_dwordx4 v77, v[242:245], s[6:7]
	ds_read_b32 v226, v214
	ds_read_b32 v227, v214 offset:512
	ds_read_b32 v228, v214 offset:1024
	ds_read_b32 v229, v214 offset:1536
	ds_read_b32 v230, v214 offset:2048
	ds_read_b32 v231, v214 offset:2560
	ds_read_b32 v232, v214 offset:3072
	ds_read_b32 v233, v214 offset:3584
	ds_read_b32 v234, v214 offset:4096
	ds_read_b32 v235, v214 offset:4608
	ds_read_b32 v236, v214 offset:5120
	ds_read_b32 v237, v214 offset:5632
	ds_read_b32 v238, v214 offset:6144
	ds_read_b32 v239, v214 offset:6656
	ds_read_b32 v240, v214 offset:7168
	ds_read_b32 v241, v214 offset:7680
	s_waitcnt lgkmcnt(0)
	v_max_f32_e32 v226, v226, v226
	v_max_f32_e32 v227, v227, v227
	v_max_f32_e32 v228, v228, v228
	v_max_f32_e32 v229, v229, v229
	v_max_f32_e32 v230, v230, v230
	v_max_f32_e32 v231, v231, v231
	v_max_f32_e32 v232, v232, v232
	v_max_f32_e32 v233, v233, v233
	v_max_f32_e32 v234, v234, v234
	v_max_f32_e32 v235, v235, v235
	v_max_f32_e32 v236, v236, v236
	v_max_f32_e32 v237, v237, v237
	v_max_f32_e32 v238, v238, v238
	v_max_f32_e32 v239, v239, v239
	v_max_f32_e32 v240, v240, v240
	v_max_f32_e32 v241, v241, v241
	v_med3_f32 v226, v226, s62, v95
	v_med3_f32 v227, v227, s62, v95
	v_med3_f32 v228, v228, s62, v95
	v_med3_f32 v229, v229, s62, v95
	v_med3_f32 v230, v230, s62, v95
	v_med3_f32 v231, v231, s62, v95
	v_med3_f32 v232, v232, s62, v95
	v_med3_f32 v233, v233, s62, v95
	v_med3_f32 v234, v234, s62, v95
	v_med3_f32 v235, v235, s62, v95
	v_med3_f32 v236, v236, s62, v95
	v_med3_f32 v237, v237, s62, v95
	v_med3_f32 v238, v238, s62, v95
	v_med3_f32 v239, v239, s62, v95
	v_med3_f32 v240, v240, s62, v95
	v_med3_f32 v241, v241, s62, v95
	v_mov_b32_e32 v242, 0
	v_mov_b32_e32 v243, 0
	v_mov_b32_e32 v244, 0
	v_mov_b32_e32 v245, 0
	v_cvt_pk_fp8_f32 v242, v226, v227
	v_cvt_pk_fp8_f32 v243, v230, v231
	v_cvt_pk_fp8_f32 v244, v234, v235
	v_cvt_pk_fp8_f32 v245, v238, v239
	v_cvt_pk_fp8_f32 v242, v228, v229 op_sel:[0,0,1]
	v_cvt_pk_fp8_f32 v243, v232, v233 op_sel:[0,0,1]
	v_cvt_pk_fp8_f32 v244, v236, v237 op_sel:[0,0,1]
	v_cvt_pk_fp8_f32 v245, v240, v241 op_sel:[0,0,1]
	s_nop 0
	global_store_dwordx4 v78, v[242:245], s[6:7]
	s_waitcnt vmcnt(12)
	v_mul_f32_e32 v144, v34, v144
	v_mul_f32_e32 v145, v34, v145
	v_mul_f32_e32 v146, v34, v146
	v_mul_f32_e32 v147, v34, v147
	ds_write_b128 v209, v[144:147]
	v_mul_f32_e32 v148, v35, v148
	v_mul_f32_e32 v149, v35, v149
	v_mul_f32_e32 v150, v35, v150
	v_mul_f32_e32 v151, v35, v151
	ds_write_b128 v209, v[148:151] offset:1024
	v_mul_f32_e32 v152, v36, v152
	v_mul_f32_e32 v153, v36, v153
	v_mul_f32_e32 v154, v36, v154
	v_mul_f32_e32 v155, v36, v155
	ds_write_b128 v209, v[152:155] offset:2048
	v_mul_f32_e32 v156, v37, v156
	v_mul_f32_e32 v157, v37, v157
	v_mul_f32_e32 v158, v37, v158
	v_mul_f32_e32 v159, v37, v159
	ds_write_b128 v209, v[156:159] offset:3072
	v_mul_f32_e32 v160, v38, v160
	v_mul_f32_e32 v161, v38, v161
	v_mul_f32_e32 v162, v38, v162
	v_mul_f32_e32 v163, v38, v163
	ds_write_b128 v209, v[160:163] offset:4096
	v_mul_f32_e32 v164, v39, v164
	v_mul_f32_e32 v165, v39, v165
	v_mul_f32_e32 v166, v39, v166
	v_mul_f32_e32 v167, v39, v167
	ds_write_b128 v209, v[164:167] offset:5120
	v_mul_f32_e32 v168, v40, v168
	v_mul_f32_e32 v169, v40, v169
	v_mul_f32_e32 v170, v40, v170
	v_mul_f32_e32 v171, v40, v171
	ds_write_b128 v209, v[168:171] offset:6144
	v_mul_f32_e32 v172, v41, v172
	v_mul_f32_e32 v173, v41, v173
	v_mul_f32_e32 v174, v41, v174
	v_mul_f32_e32 v175, v41, v175
	ds_write_b128 v209, v[172:175] offset:7168
	s_waitcnt lgkmcnt(0)
	s_barrier
; #define GAS __attribute__((address_space(1)))
; #define LAS __attribute__((address_space(3)))
; #define LDS_WAIT() asm volatile("s_waitcnt lgkmcnt(0)" ::: "memory")
;     const int pr = item >> 1, kb = 2 * (pr / nblk) + (item & 1), nb = pr % nblk, k0 = 64 * kb, n0 = 32 * nb;
;     const int nr = n0 + (lane & 31); const int sc = MAP == 1 ? src_col_in(nr) : nr;
;     float v[32];
; #pragma unroll
;     for (int i = 0; i < 32; ++i) v[i] = sc >= 0 ? W[(size_t)(k0 + 2 * i + (lane >> 5)) * Nsrc + sc] : 0.f;
; #pragma unroll
;     for (int i = 0; i < 32; ++i) { const int k = k0 + 2 * i + (lane >> 5); float x = v[i] * wscale; if (KS) x *= (k < ksplit ? ksA[k] : ksB[k - ksplit]); scr[(2 * i + (lane >> 5)) * 33 + (lane & 31)] = x; }
;     LDS_WAIT(); asm volatile("" ::: "memory");
;     const int c = lane & 7;
; #pragma unroll
;     for (int j = 0; j < 4; ++j) { const int n = (lane >> 3) + 8 * j; const LAS float* s = scr + (8 * c) * 33 + n;
;         const unsigned long long o = (unsigned long long)pg8::pk4_fp8(s[0 * 33], s[1 * 33], s[2 * 33], s[3 * 33]) | ((unsigned long long)pg8::pk4_fp8(s[4 * 33], s[5 * 33], s[6 * 33], s[7 * 33]) << 32);
;         *(GAS unsigned long long*)(WT + (size_t)(n0 + n) * K + k0 + 8 * c) = o; }
;     LDS_WAIT(); asm volatile("" ::: "memory");
; }
; __global__ void __launch_bounds__(NWAVES * 64, 2) hybrid_fwd(Args args) {
;     ...
;             if (r < I_O) { if (l >= WO_F8_FROM) p0_transpose_item_f8<true>(args.in[13] + (size_t)l * DM * DM, DM, DM, DM / 32, (unsigned char*)(ws + WS_WO + l * SZ_WO), 64.f, args.in[6] + l * 2048, args.in[12] + l * 2048, 2048, scr, r, lane);
;                 else p0_transpose_item<0, true>(args.in[13] + (size_t)l * DM * DM, DM, DM, DM / 32, (bf16*)(ws + WS_WO + l * SZ_WO), args.in[6] + l * 2048, args.in[12] + l * 2048, 2048, scr, r, lane); continue; } r -= I_O;
;             if (r < I_UP) { p0_transpose_item_f8<true>(args.in[15] + (size_t)l * DM * FF, DM, FF, FF / 32, (unsigned char*)(ws + WS_WUP + l * SZ_WUP), WUP8_SCALE, args.in[14] + l * DM, args.in[14] + l * DM, DM, scr, r, lane); continue; } r -= I_UP;
;             p0_transpose_item_f8<false>(args.in[16] + (size_t)l * FF * DM, FF, DM, DM / 32, (unsigned char*)(ws + WS_WDN + l * SZ_WDN), 128.f, args.in[16], args.in[16], 0, scr, r, lane);
	s_add_u32 s8, s34, 0xe000
	s_addc_u32 s9, s35, 0
	global_load_dwordx4 v[144:147], v74, s[8:9]
	s_add_u32 s8, s8, 0x20000
	s_addc_u32 s9, s9, 0
	global_load_dwordx4 v[148:151], v74, s[8:9]
	s_add_u32 s8, s8, 0x20000
	s_addc_u32 s9, s9, 0
	global_load_dwordx4 v[152:155], v74, s[8:9]
	s_add_u32 s8, s8, 0x20000
	s_addc_u32 s9, s9, 0
	global_load_dwordx4 v[156:159], v74, s[8:9]
	s_add_u32 s8, s8, 0x20000
	s_addc_u32 s9, s9, 0
	global_load_dwordx4 v[160:163], v74, s[8:9]
	s_add_u32 s8, s8, 0x20000
	s_addc_u32 s9, s9, 0
	global_load_dwordx4 v[164:167], v74, s[8:9]
	s_add_u32 s8, s8, 0x20000
	s_addc_u32 s9, s9, 0
	global_load_dwordx4 v[168:171], v74, s[8:9]
	s_add_u32 s8, s8, 0x20000
	s_addc_u32 s9, s9, 0
	global_load_dwordx4 v[172:175], v74, s[8:9]
	s_add_u32 s6, s36, 0x3000000
	s_addc_u32 s7, s37, 0
	ds_read_b32 v226, v211
	ds_read_b32 v227, v211 offset:512
	ds_read_b32 v228, v211 offset:1024
	ds_read_b32 v229, v211 offset:1536
	ds_read_b32 v230, v211 offset:2048
	ds_read_b32 v231, v211 offset:2560
	ds_read_b32 v232, v211 offset:3072
	ds_read_b32 v233, v211 offset:3584
	ds_read_b32 v234, v211 offset:4096
	ds_read_b32 v235, v211 offset:4608
	ds_read_b32 v236, v211 offset:5120
	ds_read_b32 v237, v211 offset:5632
	ds_read_b32 v238, v211 offset:6144
	ds_read_b32 v239, v211 offset:6656
	ds_read_b32 v240, v211 offset:7168
	ds_read_b32 v241, v211 offset:7680
	s_waitcnt lgkmcnt(0)
	v_max_f32_e32 v226, v226, v226
	v_max_f32_e32 v227, v227, v227
	v_max_f32_e32 v228, v228, v228
	v_max_f32_e32 v229, v229, v229
	v_max_f32_e32 v230, v230, v230
	v_max_f32_e32 v231, v231, v231
	v_max_f32_e32 v232, v232, v232
	v_max_f32_e32 v233, v233, v233
	v_max_f32_e32 v234, v234, v234
	v_max_f32_e32 v235, v235, v235
	v_max_f32_e32 v236, v236, v236
	v_max_f32_e32 v237, v237, v237
	v_max_f32_e32 v238, v238, v238
	v_max_f32_e32 v239, v239, v239
	v_max_f32_e32 v240, v240, v240
	v_max_f32_e32 v241, v241, v241
	v_med3_f32 v226, v226, s62, v95
	v_med3_f32 v227, v227, s62, v95
	v_med3_f32 v228, v228, s62, v95
	v_med3_f32 v229, v229, s62, v95
	v_med3_f32 v230, v230, s62, v95
	v_med3_f32 v231, v231, s62, v95
	v_med3_f32 v232, v232, s62, v95
	v_med3_f32 v233, v233, s62, v95
	v_med3_f32 v234, v234, s62, v95
	v_med3_f32 v235, v235, s62, v95
	v_med3_f32 v236, v236, s62, v95
	v_med3_f32 v237, v237, s62, v95
	v_med3_f32 v238, v238, s62, v95
	v_med3_f32 v239, v239, s62, v95
	v_med3_f32 v240, v240, s62, v95
	v_med3_f32 v241, v241, s62, v95
	v_mov_b32_e32 v242, 0
	v_mov_b32_e32 v243, 0
	v_mov_b32_e32 v244, 0
	v_mov_b32_e32 v245, 0
	v_cvt_pk_fp8_f32 v242, v226, v227
	v_cvt_pk_fp8_f32 v243, v230, v231
	v_cvt_pk_fp8_f32 v244, v234, v235
	v_cvt_pk_fp8_f32 v245, v238, v239
	v_cvt_pk_fp8_f32 v242, v228, v229 op_sel:[0,0,1]
	v_cvt_pk_fp8_f32 v243, v232, v233 op_sel:[0,0,1]
	v_cvt_pk_fp8_f32 v244, v236, v237 op_sel:[0,0,1]
	v_cvt_pk_fp8_f32 v245, v240, v241 op_sel:[0,0,1]
	s_nop 0
	global_store_dwordx4 v77, v[242:245], s[6:7]
	ds_read_b32 v226, v213
	ds_read_b32 v227, v213 offset:512
	ds_read_b32 v228, v213 offset:1024
	ds_read_b32 v229, v213 offset:1536
	ds_read_b32 v230, v213 offset:2048
	ds_read_b32 v231, v213 offset:2560
	ds_read_b32 v232, v213 offset:3072
	ds_read_b32 v233, v213 offset:3584
	ds_read_b32 v234, v213 offset:4096
	ds_read_b32 v235, v213 offset:4608
	ds_read_b32 v236, v213 offset:5120
	ds_read_b32 v237, v213 offset:5632
	ds_read_b32 v238, v213 offset:6144
	ds_read_b32 v239, v213 offset:6656
	ds_read_b32 v240, v213 offset:7168
	ds_read_b32 v241, v213 offset:7680
	s_waitcnt lgkmcnt(0)
	v_max_f32_e32 v226, v226, v226
	v_max_f32_e32 v227, v227, v227
	v_max_f32_e32 v228, v228, v228
	v_max_f32_e32 v229, v229, v229
	v_max_f32_e32 v230, v230, v230
	v_max_f32_e32 v231, v231, v231
	v_max_f32_e32 v232, v232, v232
	v_max_f32_e32 v233, v233, v233
	v_max_f32_e32 v234, v234, v234
	v_max_f32_e32 v235, v235, v235
	v_max_f32_e32 v236, v236, v236
	v_max_f32_e32 v237, v237, v237
	v_max_f32_e32 v238, v238, v238
	v_max_f32_e32 v239, v239, v239
	v_max_f32_e32 v240, v240, v240
	v_max_f32_e32 v241, v241, v241
	v_med3_f32 v226, v226, s62, v95
	v_med3_f32 v227, v227, s62, v95
	v_med3_f32 v228, v228, s62, v95
	v_med3_f32 v229, v229, s62, v95
	v_med3_f32 v230, v230, s62, v95
	v_med3_f32 v231, v231, s62, v95
	v_med3_f32 v232, v232, s62, v95
	v_med3_f32 v233, v233, s62, v95
	v_med3_f32 v234, v234, s62, v95
	v_med3_f32 v235, v235, s62, v95
	v_med3_f32 v236, v236, s62, v95
	v_med3_f32 v237, v237, s62, v95
	v_med3_f32 v238, v238, s62, v95
	v_med3_f32 v239, v239, s62, v95
	v_med3_f32 v240, v240, s62, v95
	v_med3_f32 v241, v241, s62, v95
	v_mov_b32_e32 v242, 0
	v_mov_b32_e32 v243, 0
	v_mov_b32_e32 v244, 0
	v_mov_b32_e32 v245, 0
	v_cvt_pk_fp8_f32 v242, v226, v227
	v_cvt_pk_fp8_f32 v243, v230, v231
	v_cvt_pk_fp8_f32 v244, v234, v235
	v_cvt_pk_fp8_f32 v245, v238, v239
	v_cvt_pk_fp8_f32 v242, v228, v229 op_sel:[0,0,1]
	v_cvt_pk_fp8_f32 v243, v232, v233 op_sel:[0,0,1]
	v_cvt_pk_fp8_f32 v244, v236, v237 op_sel:[0,0,1]
	v_cvt_pk_fp8_f32 v245, v240, v241 op_sel:[0,0,1]
	s_nop 0
	global_store_dwordx4 v78, v[242:245], s[6:7]
	s_waitcnt vmcnt(12)
	v_mul_f32_e32 v176, v34, v176
	v_mul_f32_e32 v177, v34, v177
	v_mul_f32_e32 v178, v34, v178
	v_mul_f32_e32 v179, v34, v179
	ds_write_b128 v210, v[176:179]
	v_mul_f32_e32 v180, v35, v180
	v_mul_f32_e32 v181, v35, v181
	v_mul_f32_e32 v182, v35, v182
	v_mul_f32_e32 v183, v35, v183
	ds_write_b128 v210, v[180:183] offset:1024
	v_mul_f32_e32 v184, v36, v184
	v_mul_f32_e32 v185, v36, v185
	v_mul_f32_e32 v186, v36, v186
	v_mul_f32_e32 v187, v36, v187
	ds_write_b128 v210, v[184:187] offset:2048
	v_mul_f32_e32 v188, v37, v188
	v_mul_f32_e32 v189, v37, v189
	v_mul_f32_e32 v190, v37, v190
	v_mul_f32_e32 v191, v37, v191
	ds_write_b128 v210, v[188:191] offset:3072
	v_mul_f32_e32 v192, v38, v192
	v_mul_f32_e32 v193, v38, v193
	v_mul_f32_e32 v194, v38, v194
	v_mul_f32_e32 v195, v38, v195
	ds_write_b128 v210, v[192:195] offset:4096
	v_mul_f32_e32 v196, v39, v196
	v_mul_f32_e32 v197, v39, v197
	v_mul_f32_e32 v198, v39, v198
	v_mul_f32_e32 v199, v39, v199
	ds_write_b128 v210, v[196:199] offset:5120
	v_mul_f32_e32 v200, v40, v200
	v_mul_f32_e32 v201, v40, v201
	v_mul_f32_e32 v202, v40, v202
	v_mul_f32_e32 v203, v40, v203
	ds_write_b128 v210, v[200:203] offset:6144
	v_mul_f32_e32 v204, v41, v204
	v_mul_f32_e32 v205, v41, v205
	v_mul_f32_e32 v206, v41, v206
	v_mul_f32_e32 v207, v41, v207
	ds_write_b128 v210, v[204:207] offset:7168
	s_waitcnt lgkmcnt(0)
	s_barrier
; #define GAS __attribute__((address_space(1)))
; #define LAS __attribute__((address_space(3)))
; #define LDS_WAIT() asm volatile("s_waitcnt lgkmcnt(0)" ::: "memory")
;     const int pr = item >> 1, kb = 2 * (pr / nblk) + (item & 1), nb = pr % nblk, k0 = 64 * kb, n0 = 32 * nb;
;     const int nr = n0 + (lane & 31); const int sc = MAP == 1 ? src_col_in(nr) : nr;
;     float v[32];
; #pragma unroll
;     for (int i = 0; i < 32; ++i) v[i] = sc >= 0 ? W[(size_t)(k0 + 2 * i + (lane >> 5)) * Nsrc + sc] : 0.f;
; #pragma unroll
;     for (int i = 0; i < 32; ++i) { const int k = k0 + 2 * i + (lane >> 5); float x = v[i] * wscale; if (KS) x *= (k < ksplit ? ksA[k] : ksB[k - ksplit]); scr[(2 * i + (lane >> 5)) * 33 + (lane & 31)] = x; }
;     LDS_WAIT(); asm volatile("" ::: "memory");
;     const int c = lane & 7;
; #pragma unroll
;     for (int j = 0; j < 4; ++j) { const int n = (lane >> 3) + 8 * j; const LAS float* s = scr + (8 * c) * 33 + n;
;         const unsigned long long o = (unsigned long long)pg8::pk4_fp8(s[0 * 33], s[1 * 33], s[2 * 33], s[3 * 33]) | ((unsigned long long)pg8::pk4_fp8(s[4 * 33], s[5 * 33], s[6 * 33], s[7 * 33]) << 32);
;         *(GAS unsigned long long*)(WT + (size_t)(n0 + n) * K + k0 + 8 * c) = o; }
;     LDS_WAIT(); asm volatile("" ::: "memory");
; }
; __global__ void __launch_bounds__(NWAVES * 64, 2) hybrid_fwd(Args args) {
;     ...
;             if (r < I_O) { if (l >= WO_F8_FROM) p0_transpose_item_f8<true>(args.in[13] + (size_t)l * DM * DM, DM, DM, DM / 32, (unsigned char*)(ws + WS_WO + l * SZ_WO), 64.f, args.in[6] + l * 2048, args.in[12] + l * 2048, 2048, scr, r, lane);
;                 else p0_transpose_item<0, true>(args.in[13] + (size_t)l * DM * DM, DM, DM, DM / 32, (bf16*)(ws + WS_WO + l * SZ_WO), args.in[6] + l * 2048, args.in[12] + l * 2048, 2048, scr, r, lane); continue; } r -= I_O;
;             if (r < I_UP) { p0_transpose_item_f8<true>(args.in[15] + (size_t)l * DM * FF, DM, FF, FF / 32, (unsigned char*)(ws + WS_WUP + l * SZ_WUP), WUP8_SCALE, args.in[14] + l * DM, args.in[14] + l * DM, DM, scr, r, lane); continue; } r -= I_UP;
;             p0_transpose_item_f8<false>(args.in[16] + (size_t)l * FF * DM, FF, DM, DM / 32, (unsigned char*)(ws + WS_WDN + l * SZ_WDN), 128.f, args.in[16], args.in[16], 0, scr, r, lane);
	s_add_u32 s8, s34, 0xf000
	s_addc_u32 s9, s35, 0
	global_load_dwordx4 v[176:179], v74, s[8:9]
	s_add_u32 s8, s8, 0x20000
	s_addc_u32 s9, s9, 0
	global_load_dwordx4 v[180:183], v74, s[8:9]
	s_add_u32 s8, s8, 0x20000
	s_addc_u32 s9, s9, 0
	global_load_dwordx4 v[184:187], v74, s[8:9]
	s_add_u32 s8, s8, 0x20000
	s_addc_u32 s9, s9, 0
	global_load_dwordx4 v[188:191], v74, s[8:9]
	s_add_u32 s8, s8, 0x20000
	s_addc_u32 s9, s9, 0
	global_load_dwordx4 v[192:195], v74, s[8:9]
	s_add_u32 s8, s8, 0x20000
	s_addc_u32 s9, s9, 0
	global_load_dwordx4 v[196:199], v74, s[8:9]
	s_add_u32 s8, s8, 0x20000
	s_addc_u32 s9, s9, 0
	global_load_dwordx4 v[200:203], v74, s[8:9]
	s_add_u32 s8, s8, 0x20000
	s_addc_u32 s9, s9, 0
	global_load_dwordx4 v[204:207], v74, s[8:9]
	s_add_u32 s6, s36, 0x3400000
	s_addc_u32 s7, s37, 0
	ds_read_b32 v226, v212
	ds_read_b32 v227, v212 offset:512
	ds_read_b32 v228, v212 offset:1024
	ds_read_b32 v229, v212 offset:1536
	ds_read_b32 v230, v212 offset:2048
	ds_read_b32 v231, v212 offset:2560
	ds_read_b32 v232, v212 offset:3072
	ds_read_b32 v233, v212 offset:3584
	ds_read_b32 v234, v212 offset:4096
	ds_read_b32 v235, v212 offset:4608
	ds_read_b32 v236, v212 offset:5120
	ds_read_b32 v237, v212 offset:5632
	ds_read_b32 v238, v212 offset:6144
	ds_read_b32 v239, v212 offset:6656
	ds_read_b32 v240, v212 offset:7168
	ds_read_b32 v241, v212 offset:7680
	s_waitcnt lgkmcnt(0)
	v_max_f32_e32 v226, v226, v226
	v_max_f32_e32 v227, v227, v227
	v_max_f32_e32 v228, v228, v228
	v_max_f32_e32 v229, v229, v229
	v_max_f32_e32 v230, v230, v230
	v_max_f32_e32 v231, v231, v231
	v_max_f32_e32 v232, v232, v232
	v_max_f32_e32 v233, v233, v233
	v_max_f32_e32 v234, v234, v234
	v_max_f32_e32 v235, v235, v235
	v_max_f32_e32 v236, v236, v236
	v_max_f32_e32 v237, v237, v237
	v_max_f32_e32 v238, v238, v238
	v_max_f32_e32 v239, v239, v239
	v_max_f32_e32 v240, v240, v240
	v_max_f32_e32 v241, v241, v241
	v_med3_f32 v226, v226, s62, v95
	v_med3_f32 v227, v227, s62, v95
	v_med3_f32 v228, v228, s62, v95
	v_med3_f32 v229, v229, s62, v95
	v_med3_f32 v230, v230, s62, v95
	v_med3_f32 v231, v231, s62, v95
	v_med3_f32 v232, v232, s62, v95
	v_med3_f32 v233, v233, s62, v95
	v_med3_f32 v234, v234, s62, v95
	v_med3_f32 v235, v235, s62, v95
	v_med3_f32 v236, v236, s62, v95
	v_med3_f32 v237, v237, s62, v95
	v_med3_f32 v238, v238, s62, v95
	v_med3_f32 v239, v239, s62, v95
	v_med3_f32 v240, v240, s62, v95
	v_med3_f32 v241, v241, s62, v95
	v_mov_b32_e32 v242, 0
	v_mov_b32_e32 v243, 0
	v_mov_b32_e32 v244, 0
	v_mov_b32_e32 v245, 0
	v_cvt_pk_fp8_f32 v242, v226, v227
	v_cvt_pk_fp8_f32 v243, v230, v231
	v_cvt_pk_fp8_f32 v244, v234, v235
	v_cvt_pk_fp8_f32 v245, v238, v239
	v_cvt_pk_fp8_f32 v242, v228, v229 op_sel:[0,0,1]
	v_cvt_pk_fp8_f32 v243, v232, v233 op_sel:[0,0,1]
	v_cvt_pk_fp8_f32 v244, v236, v237 op_sel:[0,0,1]
	v_cvt_pk_fp8_f32 v245, v240, v241 op_sel:[0,0,1]
	s_nop 0
	global_store_dwordx4 v77, v[242:245], s[6:7]
	ds_read_b32 v226, v214
	ds_read_b32 v227, v214 offset:512
	ds_read_b32 v228, v214 offset:1024
	ds_read_b32 v229, v214 offset:1536
	ds_read_b32 v230, v214 offset:2048
	ds_read_b32 v231, v214 offset:2560
	ds_read_b32 v232, v214 offset:3072
	ds_read_b32 v233, v214 offset:3584
	ds_read_b32 v234, v214 offset:4096
	ds_read_b32 v235, v214 offset:4608
	ds_read_b32 v236, v214 offset:5120
	ds_read_b32 v237, v214 offset:5632
	ds_read_b32 v238, v214 offset:6144
	ds_read_b32 v239, v214 offset:6656
	ds_read_b32 v240, v214 offset:7168
	ds_read_b32 v241, v214 offset:7680
	s_waitcnt lgkmcnt(0)
	v_max_f32_e32 v226, v226, v226
	v_max_f32_e32 v227, v227, v227
	v_max_f32_e32 v228, v228, v228
	v_max_f32_e32 v229, v229, v229
	v_max_f32_e32 v230, v230, v230
	v_max_f32_e32 v231, v231, v231
	v_max_f32_e32 v232, v232, v232
	v_max_f32_e32 v233, v233, v233
	v_max_f32_e32 v234, v234, v234
	v_max_f32_e32 v235, v235, v235
	v_max_f32_e32 v236, v236, v236
	v_max_f32_e32 v237, v237, v237
	v_max_f32_e32 v238, v238, v238
	v_max_f32_e32 v239, v239, v239
	v_max_f32_e32 v240, v240, v240
	v_max_f32_e32 v241, v241, v241
	v_med3_f32 v226, v226, s62, v95
	v_med3_f32 v227, v227, s62, v95
	v_med3_f32 v228, v228, s62, v95
	v_med3_f32 v229, v229, s62, v95
	v_med3_f32 v230, v230, s62, v95
	v_med3_f32 v231, v231, s62, v95
	v_med3_f32 v232, v232, s62, v95
	v_med3_f32 v233, v233, s62, v95
	v_med3_f32 v234, v234, s62, v95
	v_med3_f32 v235, v235, s62, v95
	v_med3_f32 v236, v236, s62, v95
	v_med3_f32 v237, v237, s62, v95
	v_med3_f32 v238, v238, s62, v95
	v_med3_f32 v239, v239, s62, v95
	v_med3_f32 v240, v240, s62, v95
	v_med3_f32 v241, v241, s62, v95
	v_mov_b32_e32 v242, 0
	v_mov_b32_e32 v243, 0
	v_mov_b32_e32 v244, 0
	v_mov_b32_e32 v245, 0
	v_cvt_pk_fp8_f32 v242, v226, v227
	v_cvt_pk_fp8_f32 v243, v230, v231
	v_cvt_pk_fp8_f32 v244, v234, v235
	v_cvt_pk_fp8_f32 v245, v238, v239
	v_cvt_pk_fp8_f32 v242, v228, v229 op_sel:[0,0,1]
	v_cvt_pk_fp8_f32 v243, v232, v233 op_sel:[0,0,1]
	v_cvt_pk_fp8_f32 v244, v236, v237 op_sel:[0,0,1]
	v_cvt_pk_fp8_f32 v245, v240, v241 op_sel:[0,0,1]
	s_nop 0
	global_store_dwordx4 v78, v[242:245], s[6:7]
	s_waitcnt vmcnt(12)
	v_mul_f32_e32 v144, v34, v144
	v_mul_f32_e32 v145, v34, v145
	v_mul_f32_e32 v146, v34, v146
	v_mul_f32_e32 v147, v34, v147
	ds_write_b128 v209, v[144:147]
	v_mul_f32_e32 v148, v35, v148
	v_mul_f32_e32 v149, v35, v149
	v_mul_f32_e32 v150, v35, v150
	v_mul_f32_e32 v151, v35, v151
	ds_write_b128 v209, v[148:151] offset:1024
	v_mul_f32_e32 v152, v36, v152
	v_mul_f32_e32 v153, v36, v153
	v_mul_f32_e32 v154, v36, v154
	v_mul_f32_e32 v155, v36, v155
	ds_write_b128 v209, v[152:155] offset:2048
	v_mul_f32_e32 v156, v37, v156
	v_mul_f32_e32 v157, v37, v157
	v_mul_f32_e32 v158, v37, v158
	v_mul_f32_e32 v159, v37, v159
	ds_write_b128 v209, v[156:159] offset:3072
	v_mul_f32_e32 v160, v38, v160
	v_mul_f32_e32 v161, v38, v161
	v_mul_f32_e32 v162, v38, v162
	v_mul_f32_e32 v163, v38, v163
	ds_write_b128 v209, v[160:163] offset:4096
	v_mul_f32_e32 v164, v39, v164
	v_mul_f32_e32 v165, v39, v165
	v_mul_f32_e32 v166, v39, v166
	v_mul_f32_e32 v167, v39, v167
	ds_write_b128 v209, v[164:167] offset:5120
	v_mul_f32_e32 v168, v40, v168
	v_mul_f32_e32 v169, v40, v169
	v_mul_f32_e32 v170, v40, v170
	v_mul_f32_e32 v171, v40, v171
	ds_write_b128 v209, v[168:171] offset:6144
	v_mul_f32_e32 v172, v41, v172
	v_mul_f32_e32 v173, v41, v173
	v_mul_f32_e32 v174, v41, v174
	v_mul_f32_e32 v175, v41, v175
	ds_write_b128 v209, v[172:175] offset:7168
	s_waitcnt lgkmcnt(0)
	s_barrier
; #define GAS __attribute__((address_space(1)))
; #define LAS __attribute__((address_space(3)))
; #define LDS_WAIT() asm volatile("s_waitcnt lgkmcnt(0)" ::: "memory")
;     const int pr = item >> 1, kb = 2 * (pr / nblk) + (item & 1), nb = pr % nblk, k0 = 64 * kb, n0 = 32 * nb;
;     const int nr = n0 + (lane & 31); const int sc = MAP == 1 ? src_col_in(nr) : nr;
;     float v[32];
; #pragma unroll
;     for (int i = 0; i < 32; ++i) v[i] = sc >= 0 ? W[(size_t)(k0 + 2 * i + (lane >> 5)) * Nsrc + sc] : 0.f;
; #pragma unroll
;     for (int i = 0; i < 32; ++i) { const int k = k0 + 2 * i + (lane >> 5); float x = v[i] * wscale; if (KS) x *= (k < ksplit ? ksA[k] : ksB[k - ksplit]); scr[(2 * i + (lane >> 5)) * 33 + (lane & 31)] = x; }
;     LDS_WAIT(); asm volatile("" ::: "memory");
;     const int c = lane & 7;
; #pragma unroll
;     for (int j = 0; j < 4; ++j) { const int n = (lane >> 3) + 8 * j; const LAS float* s = scr + (8 * c) * 33 + n;
;         const unsigned long long o = (unsigned long long)pg8::pk4_fp8(s[0 * 33], s[1 * 33], s[2 * 33], s[3 * 33]) | ((unsigned long long)pg8::pk4_fp8(s[4 * 33], s[5 * 33], s[6 * 33], s[7 * 33]) << 32);
;         *(GAS unsigned long long*)(WT + (size_t)(n0 + n) * K + k0 + 8 * c) = o; }
;     LDS_WAIT(); asm volatile("" ::: "memory");
; }
; __global__ void __launch_bounds__(NWAVES * 64, 2) hybrid_fwd(Args args) {
;     ...
;             p0_transpose_item_f8<false>(args.in[16] + (size_t)l * FF * DM, FF, DM, DM / 32, (unsigned char*)(ws + WS_WDN + l * SZ_WDN), 128.f, args.in[16], args.in[16], 0, scr, r, lane);
	s_mov_b64 s[8:9], s[38:39]
	global_load_dwordx4 v[144:147], v75, s[8:9]
	s_add_u32 s8, s8, 0x8000
	s_addc_u32 s9, s9, 0
	global_load_dwordx4 v[148:151], v75, s[8:9]
	s_add_u32 s8, s8, 0x8000
	s_addc_u32 s9, s9, 0
	global_load_dwordx4 v[152:155], v75, s[8:9]
	s_add_u32 s8, s8, 0x8000
	s_addc_u32 s9, s9, 0
	global_load_dwordx4 v[156:159], v75, s[8:9]
	s_add_u32 s8, s8, 0x8000
	s_addc_u32 s9, s9, 0
	global_load_dwordx4 v[160:163], v75, s[8:9]
	s_add_u32 s8, s8, 0x8000
	s_addc_u32 s9, s9, 0
	global_load_dwordx4 v[164:167], v75, s[8:9]
	s_add_u32 s8, s8, 0x8000
	s_addc_u32 s9, s9, 0
	global_load_dwordx4 v[168:171], v75, s[8:9]
	s_add_u32 s8, s8, 0x8000
	s_addc_u32 s9, s9, 0
	global_load_dwordx4 v[172:175], v75, s[8:9]
	s_add_u32 s6, s36, 0x3800000
	s_addc_u32 s7, s37, 0
	ds_read_b32 v226, v211
	ds_read_b32 v227, v211 offset:512
	ds_read_b32 v228, v211 offset:1024
	ds_read_b32 v229, v211 offset:1536
	ds_read_b32 v230, v211 offset:2048
	ds_read_b32 v231, v211 offset:2560
	ds_read_b32 v232, v211 offset:3072
	ds_read_b32 v233, v211 offset:3584
	ds_read_b32 v234, v211 offset:4096
	ds_read_b32 v235, v211 offset:4608
	ds_read_b32 v236, v211 offset:5120
	ds_read_b32 v237, v211 offset:5632
	ds_read_b32 v238, v211 offset:6144
	ds_read_b32 v239, v211 offset:6656
	ds_read_b32 v240, v211 offset:7168
	ds_read_b32 v241, v211 offset:7680
	s_waitcnt lgkmcnt(0)
	v_max_f32_e32 v226, v226, v226
	v_max_f32_e32 v227, v227, v227
	v_max_f32_e32 v228, v228, v228
	v_max_f32_e32 v229, v229, v229
	v_max_f32_e32 v230, v230, v230
	v_max_f32_e32 v231, v231, v231
	v_max_f32_e32 v232, v232, v232
	v_max_f32_e32 v233, v233, v233
	v_max_f32_e32 v234, v234, v234
	v_max_f32_e32 v235, v235, v235
	v_max_f32_e32 v236, v236, v236
	v_max_f32_e32 v237, v237, v237
	v_max_f32_e32 v238, v238, v238
	v_max_f32_e32 v239, v239, v239
	v_max_f32_e32 v240, v240, v240
	v_max_f32_e32 v241, v241, v241
	v_med3_f32 v226, v226, s62, v95
	v_med3_f32 v227, v227, s62, v95
	v_med3_f32 v228, v228, s62, v95
	v_med3_f32 v229, v229, s62, v95
	v_med3_f32 v230, v230, s62, v95
	v_med3_f32 v231, v231, s62, v95
	v_med3_f32 v232, v232, s62, v95
	v_med3_f32 v233, v233, s62, v95
	v_med3_f32 v234, v234, s62, v95
	v_med3_f32 v235, v235, s62, v95
	v_med3_f32 v236, v236, s62, v95
	v_med3_f32 v237, v237, s62, v95
	v_med3_f32 v238, v238, s62, v95
	v_med3_f32 v239, v239, s62, v95
	v_med3_f32 v240, v240, s62, v95
	v_med3_f32 v241, v241, s62, v95
	v_mov_b32_e32 v242, 0
	v_mov_b32_e32 v243, 0
	v_mov_b32_e32 v244, 0
	v_mov_b32_e32 v245, 0
	v_cvt_pk_fp8_f32 v242, v226, v227
	v_cvt_pk_fp8_f32 v243, v230, v231
	v_cvt_pk_fp8_f32 v244, v234, v235
	v_cvt_pk_fp8_f32 v245, v238, v239
	v_cvt_pk_fp8_f32 v242, v228, v229 op_sel:[0,0,1]
	v_cvt_pk_fp8_f32 v243, v232, v233 op_sel:[0,0,1]
	v_cvt_pk_fp8_f32 v244, v236, v237 op_sel:[0,0,1]
	v_cvt_pk_fp8_f32 v245, v240, v241 op_sel:[0,0,1]
	s_nop 0
	global_store_dwordx4 v77, v[242:245], s[6:7]
	ds_read_b32 v226, v213
	ds_read_b32 v227, v213 offset:512
	ds_read_b32 v228, v213 offset:1024
	ds_read_b32 v229, v213 offset:1536
	ds_read_b32 v230, v213 offset:2048
	ds_read_b32 v231, v213 offset:2560
	ds_read_b32 v232, v213 offset:3072
	ds_read_b32 v233, v213 offset:3584
	ds_read_b32 v234, v213 offset:4096
	ds_read_b32 v235, v213 offset:4608
	ds_read_b32 v236, v213 offset:5120
	ds_read_b32 v237, v213 offset:5632
	ds_read_b32 v238, v213 offset:6144
	ds_read_b32 v239, v213 offset:6656
	ds_read_b32 v240, v213 offset:7168
	ds_read_b32 v241, v213 offset:7680
	s_waitcnt lgkmcnt(0)
	v_max_f32_e32 v226, v226, v226
	v_max_f32_e32 v227, v227, v227
	v_max_f32_e32 v228, v228, v228
	v_max_f32_e32 v229, v229, v229
	v_max_f32_e32 v230, v230, v230
	v_max_f32_e32 v231, v231, v231
	v_max_f32_e32 v232, v232, v232
	v_max_f32_e32 v233, v233, v233
	v_max_f32_e32 v234, v234, v234
	v_max_f32_e32 v235, v235, v235
	v_max_f32_e32 v236, v236, v236
	v_max_f32_e32 v237, v237, v237
	v_max_f32_e32 v238, v238, v238
	v_max_f32_e32 v239, v239, v239
	v_max_f32_e32 v240, v240, v240
	v_max_f32_e32 v241, v241, v241
	v_med3_f32 v226, v226, s62, v95
	v_med3_f32 v227, v227, s62, v95
	v_med3_f32 v228, v228, s62, v95
	v_med3_f32 v229, v229, s62, v95
	v_med3_f32 v230, v230, s62, v95
	v_med3_f32 v231, v231, s62, v95
	v_med3_f32 v232, v232, s62, v95
	v_med3_f32 v233, v233, s62, v95
	v_med3_f32 v234, v234, s62, v95
	v_med3_f32 v235, v235, s62, v95
	v_med3_f32 v236, v236, s62, v95
	v_med3_f32 v237, v237, s62, v95
	v_med3_f32 v238, v238, s62, v95
	v_med3_f32 v239, v239, s62, v95
	v_med3_f32 v240, v240, s62, v95
	v_med3_f32 v241, v241, s62, v95
	v_mov_b32_e32 v242, 0
	v_mov_b32_e32 v243, 0
	v_mov_b32_e32 v244, 0
	v_mov_b32_e32 v245, 0
	v_cvt_pk_fp8_f32 v242, v226, v227
	v_cvt_pk_fp8_f32 v243, v230, v231
	v_cvt_pk_fp8_f32 v244, v234, v235
	v_cvt_pk_fp8_f32 v245, v238, v239
	v_cvt_pk_fp8_f32 v242, v228, v229 op_sel:[0,0,1]
	v_cvt_pk_fp8_f32 v243, v232, v233 op_sel:[0,0,1]
	v_cvt_pk_fp8_f32 v244, v236, v237 op_sel:[0,0,1]
	v_cvt_pk_fp8_f32 v245, v240, v241 op_sel:[0,0,1]
	s_nop 0
	global_store_dwordx4 v78, v[242:245], s[6:7]
	s_waitcnt vmcnt(12)
	v_mul_f32_e32 v176, v34, v176
	v_mul_f32_e32 v177, v34, v177
	v_mul_f32_e32 v178, v34, v178
	v_mul_f32_e32 v179, v34, v179
	ds_write_b128 v210, v[176:179]
	v_mul_f32_e32 v180, v35, v180
	v_mul_f32_e32 v181, v35, v181
	v_mul_f32_e32 v182, v35, v182
	v_mul_f32_e32 v183, v35, v183
	ds_write_b128 v210, v[180:183] offset:1024
	v_mul_f32_e32 v184, v36, v184
	v_mul_f32_e32 v185, v36, v185
	v_mul_f32_e32 v186, v36, v186
	v_mul_f32_e32 v187, v36, v187
	ds_write_b128 v210, v[184:187] offset:2048
	v_mul_f32_e32 v188, v37, v188
	v_mul_f32_e32 v189, v37, v189
	v_mul_f32_e32 v190, v37, v190
	v_mul_f32_e32 v191, v37, v191
	ds_write_b128 v210, v[188:191] offset:3072
	v_mul_f32_e32 v192, v38, v192
	v_mul_f32_e32 v193, v38, v193
	v_mul_f32_e32 v194, v38, v194
	v_mul_f32_e32 v195, v38, v195
	ds_write_b128 v210, v[192:195] offset:4096
	v_mul_f32_e32 v196, v39, v196
	v_mul_f32_e32 v197, v39, v197
	v_mul_f32_e32 v198, v39, v198
	v_mul_f32_e32 v199, v39, v199
	ds_write_b128 v210, v[196:199] offset:5120
	v_mul_f32_e32 v200, v40, v200
	v_mul_f32_e32 v201, v40, v201
	v_mul_f32_e32 v202, v40, v202
	v_mul_f32_e32 v203, v40, v203
	ds_write_b128 v210, v[200:203] offset:6144
	v_mul_f32_e32 v204, v41, v204
	v_mul_f32_e32 v205, v41, v205
	v_mul_f32_e32 v206, v41, v206
	v_mul_f32_e32 v207, v41, v207
	ds_write_b128 v210, v[204:207] offset:7168
	s_waitcnt lgkmcnt(0)
	s_barrier
; #define GAS __attribute__((address_space(1)))
; #define LAS __attribute__((address_space(3)))
; #define LDS_WAIT() asm volatile("s_waitcnt lgkmcnt(0)" ::: "memory")
;     const int pr = item >> 1, kb = 2 * (pr / nblk) + (item & 1), nb = pr % nblk, k0 = 64 * kb, n0 = 32 * nb;
;     const int nr = n0 + (lane & 31); const int sc = MAP == 1 ? src_col_in(nr) : nr;
;     float v[32];
; #pragma unroll
;     for (int i = 0; i < 32; ++i) v[i] = sc >= 0 ? W[(size_t)(k0 + 2 * i + (lane >> 5)) * Nsrc + sc] : 0.f;
; #pragma unroll
;     for (int i = 0; i < 32; ++i) { const int k = k0 + 2 * i + (lane >> 5); float x = v[i] * wscale; if (KS) x *= (k < ksplit ? ksA[k] : ksB[k - ksplit]); scr[(2 * i + (lane >> 5)) * 33 + (lane & 31)] = x; }
;     LDS_WAIT(); asm volatile("" ::: "memory");
;     const int c = lane & 7;
; #pragma unroll
;     for (int j = 0; j < 4; ++j) { const int n = (lane >> 3) + 8 * j; const LAS float* s = scr + (8 * c) * 33 + n;
;         const unsigned long long o = (unsigned long long)pg8::pk4_fp8(s[0 * 33], s[1 * 33], s[2 * 33], s[3 * 33]) | ((unsigned long long)pg8::pk4_fp8(s[4 * 33], s[5 * 33], s[6 * 33], s[7 * 33]) << 32);
;         *(GAS unsigned long long*)(WT + (size_t)(n0 + n) * K + k0 + 8 * c) = o; }
;     LDS_WAIT(); asm volatile("" ::: "memory");
; }
; __global__ void __launch_bounds__(NWAVES * 64, 2) hybrid_fwd(Args args) {
;     ...
;             p0_transpose_item_f8<false>(args.in[16] + (size_t)l * FF * DM, FF, DM, DM / 32, (unsigned char*)(ws + WS_WDN + l * SZ_WDN), 128.f, args.in[16], args.in[16], 0, scr, r, lane);
	s_add_u32 s8, s38, 0x1000
	s_addc_u32 s9, s39, 0
	global_load_dwordx4 v[176:179], v75, s[8:9]
	s_add_u32 s8, s8, 0x8000
	s_addc_u32 s9, s9, 0
	global_load_dwordx4 v[180:183], v75, s[8:9]
	s_add_u32 s8, s8, 0x8000
	s_addc_u32 s9, s9, 0
	global_load_dwordx4 v[184:187], v75, s[8:9]
	s_add_u32 s8, s8, 0x8000
	s_addc_u32 s9, s9, 0
	global_load_dwordx4 v[188:191], v75, s[8:9]
	s_add_u32 s8, s8, 0x8000
	s_addc_u32 s9, s9, 0
	global_load_dwordx4 v[192:195], v75, s[8:9]
	s_add_u32 s8, s8, 0x8000
	s_addc_u32 s9, s9, 0
	global_load_dwordx4 v[196:199], v75, s[8:9]
	s_add_u32 s8, s8, 0x8000
	s_addc_u32 s9, s9, 0
	global_load_dwordx4 v[200:203], v75, s[8:9]
	s_add_u32 s8, s8, 0x8000
	s_addc_u32 s9, s9, 0
	global_load_dwordx4 v[204:207], v75, s[8:9]
	s_add_u32 s6, s36, 0x3c00000
	s_addc_u32 s7, s37, 0
	ds_read_b32 v226, v212
	ds_read_b32 v227, v212 offset:512
	ds_read_b32 v228, v212 offset:1024
	ds_read_b32 v229, v212 offset:1536
	ds_read_b32 v230, v212 offset:2048
	ds_read_b32 v231, v212 offset:2560
	ds_read_b32 v232, v212 offset:3072
	ds_read_b32 v233, v212 offset:3584
	ds_read_b32 v234, v212 offset:4096
	ds_read_b32 v235, v212 offset:4608
	ds_read_b32 v236, v212 offset:5120
	ds_read_b32 v237, v212 offset:5632
	ds_read_b32 v238, v212 offset:6144
	ds_read_b32 v239, v212 offset:6656
	ds_read_b32 v240, v212 offset:7168
	ds_read_b32 v241, v212 offset:7680
	s_waitcnt lgkmcnt(0)
	v_max_f32_e32 v226, v226, v226
	v_max_f32_e32 v227, v227, v227
	v_max_f32_e32 v228, v228, v228
	v_max_f32_e32 v229, v229, v229
	v_max_f32_e32 v230, v230, v230
	v_max_f32_e32 v231, v231, v231
	v_max_f32_e32 v232, v232, v232
	v_max_f32_e32 v233, v233, v233
	v_max_f32_e32 v234, v234, v234
	v_max_f32_e32 v235, v235, v235
	v_max_f32_e32 v236, v236, v236
	v_max_f32_e32 v237, v237, v237
	v_max_f32_e32 v238, v238, v238
	v_max_f32_e32 v239, v239, v239
	v_max_f32_e32 v240, v240, v240
	v_max_f32_e32 v241, v241, v241
	v_med3_f32 v226, v226, s62, v95
	v_med3_f32 v227, v227, s62, v95
	v_med3_f32 v228, v228, s62, v95
	v_med3_f32 v229, v229, s62, v95
	v_med3_f32 v230, v230, s62, v95
	v_med3_f32 v231, v231, s62, v95
	v_med3_f32 v232, v232, s62, v95
	v_med3_f32 v233, v233, s62, v95
	v_med3_f32 v234, v234, s62, v95
	v_med3_f32 v235, v235, s62, v95
	v_med3_f32 v236, v236, s62, v95
	v_med3_f32 v237, v237, s62, v95
	v_med3_f32 v238, v238, s62, v95
	v_med3_f32 v239, v239, s62, v95
	v_med3_f32 v240, v240, s62, v95
	v_med3_f32 v241, v241, s62, v95
	v_mov_b32_e32 v242, 0
	v_mov_b32_e32 v243, 0
	v_mov_b32_e32 v244, 0
	v_mov_b32_e32 v245, 0
	v_cvt_pk_fp8_f32 v242, v226, v227
	v_cvt_pk_fp8_f32 v243, v230, v231
	v_cvt_pk_fp8_f32 v244, v234, v235
	v_cvt_pk_fp8_f32 v245, v238, v239
	v_cvt_pk_fp8_f32 v242, v228, v229 op_sel:[0,0,1]
	v_cvt_pk_fp8_f32 v243, v232, v233 op_sel:[0,0,1]
	v_cvt_pk_fp8_f32 v244, v236, v237 op_sel:[0,0,1]
	v_cvt_pk_fp8_f32 v245, v240, v241 op_sel:[0,0,1]
	s_nop 0
	global_store_dwordx4 v77, v[242:245], s[6:7]
	ds_read_b32 v226, v214
	ds_read_b32 v227, v214 offset:512
	ds_read_b32 v228, v214 offset:1024
	ds_read_b32 v229, v214 offset:1536
	ds_read_b32 v230, v214 offset:2048
	ds_read_b32 v231, v214 offset:2560
	ds_read_b32 v232, v214 offset:3072
	ds_read_b32 v233, v214 offset:3584
	ds_read_b32 v234, v214 offset:4096
	ds_read_b32 v235, v214 offset:4608
	ds_read_b32 v236, v214 offset:5120
	ds_read_b32 v237, v214 offset:5632
	ds_read_b32 v238, v214 offset:6144
	ds_read_b32 v239, v214 offset:6656
	ds_read_b32 v240, v214 offset:7168
	ds_read_b32 v241, v214 offset:7680
	s_waitcnt lgkmcnt(0)
	v_max_f32_e32 v226, v226, v226
	v_max_f32_e32 v227, v227, v227
	v_max_f32_e32 v228, v228, v228
	v_max_f32_e32 v229, v229, v229
	v_max_f32_e32 v230, v230, v230
	v_max_f32_e32 v231, v231, v231
	v_max_f32_e32 v232, v232, v232
	v_max_f32_e32 v233, v233, v233
	v_max_f32_e32 v234, v234, v234
	v_max_f32_e32 v235, v235, v235
	v_max_f32_e32 v236, v236, v236
	v_max_f32_e32 v237, v237, v237
	v_max_f32_e32 v238, v238, v238
	v_max_f32_e32 v239, v239, v239
	v_max_f32_e32 v240, v240, v240
	v_max_f32_e32 v241, v241, v241
	v_med3_f32 v226, v226, s62, v95
	v_med3_f32 v227, v227, s62, v95
	v_med3_f32 v228, v228, s62, v95
	v_med3_f32 v229, v229, s62, v95
	v_med3_f32 v230, v230, s62, v95
	v_med3_f32 v231, v231, s62, v95
	v_med3_f32 v232, v232, s62, v95
	v_med3_f32 v233, v233, s62, v95
	v_med3_f32 v234, v234, s62, v95
	v_med3_f32 v235, v235, s62, v95
	v_med3_f32 v236, v236, s62, v95
	v_med3_f32 v237, v237, s62, v95
	v_med3_f32 v238, v238, s62, v95
	v_med3_f32 v239, v239, s62, v95
	v_med3_f32 v240, v240, s62, v95
	v_med3_f32 v241, v241, s62, v95
	v_mov_b32_e32 v242, 0
	v_mov_b32_e32 v243, 0
	v_mov_b32_e32 v244, 0
	v_mov_b32_e32 v245, 0
	v_cvt_pk_fp8_f32 v242, v226, v227
	v_cvt_pk_fp8_f32 v243, v230, v231
	v_cvt_pk_fp8_f32 v244, v234, v235
	v_cvt_pk_fp8_f32 v245, v238, v239
	v_cvt_pk_fp8_f32 v242, v228, v229 op_sel:[0,0,1]
	v_cvt_pk_fp8_f32 v243, v232, v233 op_sel:[0,0,1]
	v_cvt_pk_fp8_f32 v244, v236, v237 op_sel:[0,0,1]
	v_cvt_pk_fp8_f32 v245, v240, v241 op_sel:[0,0,1]
	s_nop 0
	global_store_dwordx4 v78, v[242:245], s[6:7]
	s_waitcnt vmcnt(12)
	v_mul_f32_e32 v144, 0x43000000, v144
	v_mul_f32_e32 v145, 0x43000000, v145
	v_mul_f32_e32 v146, 0x43000000, v146
	v_mul_f32_e32 v147, 0x43000000, v147
	ds_write_b128 v209, v[144:147]
	v_mul_f32_e32 v148, 0x43000000, v148
	v_mul_f32_e32 v149, 0x43000000, v149
	v_mul_f32_e32 v150, 0x43000000, v150
	v_mul_f32_e32 v151, 0x43000000, v151
	ds_write_b128 v209, v[148:151] offset:1024
	v_mul_f32_e32 v152, 0x43000000, v152
	v_mul_f32_e32 v153, 0x43000000, v153
	v_mul_f32_e32 v154, 0x43000000, v154
	v_mul_f32_e32 v155, 0x43000000, v155
	ds_write_b128 v209, v[152:155] offset:2048
	v_mul_f32_e32 v156, 0x43000000, v156
	v_mul_f32_e32 v157, 0x43000000, v157
	v_mul_f32_e32 v158, 0x43000000, v158
	v_mul_f32_e32 v159, 0x43000000, v159
	ds_write_b128 v209, v[156:159] offset:3072
	v_mul_f32_e32 v160, 0x43000000, v160
	v_mul_f32_e32 v161, 0x43000000, v161
	v_mul_f32_e32 v162, 0x43000000, v162
	v_mul_f32_e32 v163, 0x43000000, v163
	ds_write_b128 v209, v[160:163] offset:4096
	v_mul_f32_e32 v164, 0x43000000, v164
	v_mul_f32_e32 v165, 0x43000000, v165
	v_mul_f32_e32 v166, 0x43000000, v166
	v_mul_f32_e32 v167, 0x43000000, v167
	ds_write_b128 v209, v[164:167] offset:5120
	v_mul_f32_e32 v168, 0x43000000, v168
	v_mul_f32_e32 v169, 0x43000000, v169
	v_mul_f32_e32 v170, 0x43000000, v170
	v_mul_f32_e32 v171, 0x43000000, v171
	ds_write_b128 v209, v[168:171] offset:6144
	v_mul_f32_e32 v172, 0x43000000, v172
	v_mul_f32_e32 v173, 0x43000000, v173
	v_mul_f32_e32 v174, 0x43000000, v174
	v_mul_f32_e32 v175, 0x43000000, v175
	ds_write_b128 v209, v[172:175] offset:7168
	s_waitcnt lgkmcnt(0)
	s_barrier
; #define GAS __attribute__((address_space(1)))
; #define LAS __attribute__((address_space(3)))
; #define LDS_WAIT() asm volatile("s_waitcnt lgkmcnt(0)" ::: "memory")
;     const int pr = item >> 1, kb = 2 * (pr / nblk) + (item & 1), nb = pr % nblk, k0 = 64 * kb, n0 = 32 * nb;
;     const int nr = n0 + (lane & 31); const int sc = MAP == 1 ? src_col_in(nr) : nr;
;     float v[32];
; #pragma unroll
;     for (int i = 0; i < 32; ++i) v[i] = sc >= 0 ? W[(size_t)(k0 + 2 * i + (lane >> 5)) * Nsrc + sc] : 0.f;
; #pragma unroll
;     for (int i = 0; i < 32; ++i) { const int k = k0 + 2 * i + (lane >> 5); float x = v[i] * wscale; if (KS) x *= (k < ksplit ? ksA[k] : ksB[k - ksplit]); scr[(2 * i + (lane >> 5)) * 33 + (lane & 31)] = x; }
;     LDS_WAIT(); asm volatile("" ::: "memory");
;     const int c = lane & 7;
; #pragma unroll
;     for (int j = 0; j < 4; ++j) { const int n = (lane >> 3) + 8 * j; const LAS float* s = scr + (8 * c) * 33 + n;
;         const unsigned long long o = (unsigned long long)pg8::pk4_fp8(s[0 * 33], s[1 * 33], s[2 * 33], s[3 * 33]) | ((unsigned long long)pg8::pk4_fp8(s[4 * 33], s[5 * 33], s[6 * 33], s[7 * 33]) << 32);
;         *(GAS unsigned long long*)(WT + (size_t)(n0 + n) * K + k0 + 8 * c) = o; }
;     LDS_WAIT(); asm volatile("" ::: "memory");
; }
; __global__ void __launch_bounds__(NWAVES * 64, 2) hybrid_fwd(Args args) {
;     ...
;             p0_transpose_item_f8<false>(args.in[16] + (size_t)l * FF * DM, FF, DM, DM / 32, (unsigned char*)(ws + WS_WDN + l * SZ_WDN), 128.f, args.in[16], args.in[16], 0, scr, r, lane);
	s_add_u32 s8, s38, 0x2000
	s_addc_u32 s9, s39, 0
	global_load_dwordx4 v[144:147], v75, s[8:9]
	s_add_u32 s8, s8, 0x8000
	s_addc_u32 s9, s9, 0
	global_load_dwordx4 v[148:151], v75, s[8:9]
	s_add_u32 s8, s8, 0x8000
	s_addc_u32 s9, s9, 0
	global_load_dwordx4 v[152:155], v75, s[8:9]
	s_add_u32 s8, s8, 0x8000
	s_addc_u32 s9, s9, 0
	global_load_dwordx4 v[156:159], v75, s[8:9]
	s_add_u32 s8, s8, 0x8000
	s_addc_u32 s9, s9, 0
	global_load_dwordx4 v[160:163], v75, s[8:9]
	s_add_u32 s8, s8, 0x8000
	s_addc_u32 s9, s9, 0
	global_load_dwordx4 v[164:167], v75, s[8:9]
	s_add_u32 s8, s8, 0x8000
	s_addc_u32 s9, s9, 0
	global_load_dwordx4 v[168:171], v75, s[8:9]
	s_add_u32 s8, s8, 0x8000
	s_addc_u32 s9, s9, 0
	global_load_dwordx4 v[172:175], v75, s[8:9]
	s_mov_b64 s[6:7], s[40:41]
	ds_read_b32 v226, v211
	ds_read_b32 v227, v211 offset:512
	ds_read_b32 v228, v211 offset:1024
	ds_read_b32 v229, v211 offset:1536
	ds_read_b32 v230, v211 offset:2048
	ds_read_b32 v231, v211 offset:2560
	ds_read_b32 v232, v211 offset:3072
	ds_read_b32 v233, v211 offset:3584
	ds_read_b32 v234, v211 offset:4096
	ds_read_b32 v235, v211 offset:4608
	ds_read_b32 v236, v211 offset:5120
	ds_read_b32 v237, v211 offset:5632
	ds_read_b32 v238, v211 offset:6144
	ds_read_b32 v239, v211 offset:6656
	ds_read_b32 v240, v211 offset:7168
	ds_read_b32 v241, v211 offset:7680
	s_waitcnt lgkmcnt(0)
	v_max_f32_e32 v226, v226, v226
	v_max_f32_e32 v227, v227, v227
	v_max_f32_e32 v228, v228, v228
	v_max_f32_e32 v229, v229, v229
	v_max_f32_e32 v230, v230, v230
	v_max_f32_e32 v231, v231, v231
	v_max_f32_e32 v232, v232, v232
	v_max_f32_e32 v233, v233, v233
	v_max_f32_e32 v234, v234, v234
	v_max_f32_e32 v235, v235, v235
	v_max_f32_e32 v236, v236, v236
	v_max_f32_e32 v237, v237, v237
	v_max_f32_e32 v238, v238, v238
	v_max_f32_e32 v239, v239, v239
	v_max_f32_e32 v240, v240, v240
	v_max_f32_e32 v241, v241, v241
	v_med3_f32 v226, v226, s62, v95
	v_med3_f32 v227, v227, s62, v95
	v_med3_f32 v228, v228, s62, v95
	v_med3_f32 v229, v229, s62, v95
	v_med3_f32 v230, v230, s62, v95
	v_med3_f32 v231, v231, s62, v95
	v_med3_f32 v232, v232, s62, v95
	v_med3_f32 v233, v233, s62, v95
	v_med3_f32 v234, v234, s62, v95
	v_med3_f32 v235, v235, s62, v95
	v_med3_f32 v236, v236, s62, v95
	v_med3_f32 v237, v237, s62, v95
	v_med3_f32 v238, v238, s62, v95
	v_med3_f32 v239, v239, s62, v95
	v_med3_f32 v240, v240, s62, v95
	v_med3_f32 v241, v241, s62, v95
	v_mov_b32_e32 v242, 0
	v_mov_b32_e32 v243, 0
	v_mov_b32_e32 v244, 0
	v_mov_b32_e32 v245, 0
	v_cvt_pk_fp8_f32 v242, v226, v227
	v_cvt_pk_fp8_f32 v243, v230, v231
	v_cvt_pk_fp8_f32 v244, v234, v235
	v_cvt_pk_fp8_f32 v245, v238, v239
	v_cvt_pk_fp8_f32 v242, v228, v229 op_sel:[0,0,1]
	v_cvt_pk_fp8_f32 v243, v232, v233 op_sel:[0,0,1]
	v_cvt_pk_fp8_f32 v244, v236, v237 op_sel:[0,0,1]
	v_cvt_pk_fp8_f32 v245, v240, v241 op_sel:[0,0,1]
	s_nop 0
	global_store_dwordx4 v79, v[242:245], s[6:7]
	ds_read_b32 v226, v213
	ds_read_b32 v227, v213 offset:512
	ds_read_b32 v228, v213 offset:1024
	ds_read_b32 v229, v213 offset:1536
	ds_read_b32 v230, v213 offset:2048
	ds_read_b32 v231, v213 offset:2560
	ds_read_b32 v232, v213 offset:3072
	ds_read_b32 v233, v213 offset:3584
	ds_read_b32 v234, v213 offset:4096
	ds_read_b32 v235, v213 offset:4608
	ds_read_b32 v236, v213 offset:5120
	ds_read_b32 v237, v213 offset:5632
	ds_read_b32 v238, v213 offset:6144
	ds_read_b32 v239, v213 offset:6656
	ds_read_b32 v240, v213 offset:7168
	ds_read_b32 v241, v213 offset:7680
	s_waitcnt lgkmcnt(0)
	v_max_f32_e32 v226, v226, v226
	v_max_f32_e32 v227, v227, v227
	v_max_f32_e32 v228, v228, v228
	v_max_f32_e32 v229, v229, v229
	v_max_f32_e32 v230, v230, v230
	v_max_f32_e32 v231, v231, v231
	v_max_f32_e32 v232, v232, v232
	v_max_f32_e32 v233, v233, v233
	v_max_f32_e32 v234, v234, v234
	v_max_f32_e32 v235, v235, v235
	v_max_f32_e32 v236, v236, v236
	v_max_f32_e32 v237, v237, v237
	v_max_f32_e32 v238, v238, v238
	v_max_f32_e32 v239, v239, v239
	v_max_f32_e32 v240, v240, v240
	v_max_f32_e32 v241, v241, v241
	v_med3_f32 v226, v226, s62, v95
	v_med3_f32 v227, v227, s62, v95
	v_med3_f32 v228, v228, s62, v95
	v_med3_f32 v229, v229, s62, v95
	v_med3_f32 v230, v230, s62, v95
	v_med3_f32 v231, v231, s62, v95
	v_med3_f32 v232, v232, s62, v95
	v_med3_f32 v233, v233, s62, v95
	v_med3_f32 v234, v234, s62, v95
	v_med3_f32 v235, v235, s62, v95
	v_med3_f32 v236, v236, s62, v95
	v_med3_f32 v237, v237, s62, v95
	v_med3_f32 v238, v238, s62, v95
	v_med3_f32 v239, v239, s62, v95
	v_med3_f32 v240, v240, s62, v95
	v_med3_f32 v241, v241, s62, v95
	v_mov_b32_e32 v242, 0
	v_mov_b32_e32 v243, 0
	v_mov_b32_e32 v244, 0
	v_mov_b32_e32 v245, 0
	v_cvt_pk_fp8_f32 v242, v226, v227
	v_cvt_pk_fp8_f32 v243, v230, v231
	v_cvt_pk_fp8_f32 v244, v234, v235
	v_cvt_pk_fp8_f32 v245, v238, v239
	v_cvt_pk_fp8_f32 v242, v228, v229 op_sel:[0,0,1]
	v_cvt_pk_fp8_f32 v243, v232, v233 op_sel:[0,0,1]
	v_cvt_pk_fp8_f32 v244, v236, v237 op_sel:[0,0,1]
	v_cvt_pk_fp8_f32 v245, v240, v241 op_sel:[0,0,1]
	s_nop 0
	global_store_dwordx4 v80, v[242:245], s[6:7]
	s_waitcnt vmcnt(12)
	v_mul_f32_e32 v176, 0x43000000, v176
	v_mul_f32_e32 v177, 0x43000000, v177
	v_mul_f32_e32 v178, 0x43000000, v178
	v_mul_f32_e32 v179, 0x43000000, v179
	ds_write_b128 v210, v[176:179]
	v_mul_f32_e32 v180, 0x43000000, v180
	v_mul_f32_e32 v181, 0x43000000, v181
	v_mul_f32_e32 v182, 0x43000000, v182
	v_mul_f32_e32 v183, 0x43000000, v183
	ds_write_b128 v210, v[180:183] offset:1024
	v_mul_f32_e32 v184, 0x43000000, v184
	v_mul_f32_e32 v185, 0x43000000, v185
	v_mul_f32_e32 v186, 0x43000000, v186
	v_mul_f32_e32 v187, 0x43000000, v187
	ds_write_b128 v210, v[184:187] offset:2048
	v_mul_f32_e32 v188, 0x43000000, v188
	v_mul_f32_e32 v189, 0x43000000, v189
	v_mul_f32_e32 v190, 0x43000000, v190
	v_mul_f32_e32 v191, 0x43000000, v191
	ds_write_b128 v210, v[188:191] offset:3072
	v_mul_f32_e32 v192, 0x43000000, v192
	v_mul_f32_e32 v193, 0x43000000, v193
	v_mul_f32_e32 v194, 0x43000000, v194
	v_mul_f32_e32 v195, 0x43000000, v195
	ds_write_b128 v210, v[192:195] offset:4096
	v_mul_f32_e32 v196, 0x43000000, v196
	v_mul_f32_e32 v197, 0x43000000, v197
	v_mul_f32_e32 v198, 0x43000000, v198
	v_mul_f32_e32 v199, 0x43000000, v199
	ds_write_b128 v210, v[196:199] offset:5120
	v_mul_f32_e32 v200, 0x43000000, v200
	v_mul_f32_e32 v201, 0x43000000, v201
	v_mul_f32_e32 v202, 0x43000000, v202
	v_mul_f32_e32 v203, 0x43000000, v203
	ds_write_b128 v210, v[200:203] offset:6144
	v_mul_f32_e32 v204, 0x43000000, v204
	v_mul_f32_e32 v205, 0x43000000, v205
	v_mul_f32_e32 v206, 0x43000000, v206
	v_mul_f32_e32 v207, 0x43000000, v207
	ds_write_b128 v210, v[204:207] offset:7168
	s_waitcnt lgkmcnt(0)
	s_barrier
; #define GAS __attribute__((address_space(1)))
; #define LAS __attribute__((address_space(3)))
; #define LDS_WAIT() asm volatile("s_waitcnt lgkmcnt(0)" ::: "memory")
;     const int pr = item >> 1, kb = 2 * (pr / nblk) + (item & 1), nb = pr % nblk, k0 = 64 * kb, n0 = 32 * nb;
;     const int nr = n0 + (lane & 31); const int sc = MAP == 1 ? src_col_in(nr) : nr;
;     float v[32];
; #pragma unroll
;     for (int i = 0; i < 32; ++i) v[i] = sc >= 0 ? W[(size_t)(k0 + 2 * i + (lane >> 5)) * Nsrc + sc] : 0.f;
; #pragma unroll
;     for (int i = 0; i < 32; ++i) { const int k = k0 + 2 * i + (lane >> 5); float x = v[i] * wscale; if (KS) x *= (k < ksplit ? ksA[k] : ksB[k - ksplit]); scr[(2 * i + (lane >> 5)) * 33 + (lane & 31)] = x; }
;     LDS_WAIT(); asm volatile("" ::: "memory");
;     const int c = lane & 7;
; #pragma unroll
;     for (int j = 0; j < 4; ++j) { const int n = (lane >> 3) + 8 * j; const LAS float* s = scr + (8 * c) * 33 + n;
;         const unsigned long long o = (unsigned long long)pg8::pk4_fp8(s[0 * 33], s[1 * 33], s[2 * 33], s[3 * 33]) | ((unsigned long long)pg8::pk4_fp8(s[4 * 33], s[5 * 33], s[6 * 33], s[7 * 33]) << 32);
;         *(GAS unsigned long long*)(WT + (size_t)(n0 + n) * K + k0 + 8 * c) = o; }
;     LDS_WAIT(); asm volatile("" ::: "memory");
; }
; __global__ void __launch_bounds__(NWAVES * 64, 2) hybrid_fwd(Args args) {
;     ...
;             p0_transpose_item_f8<false>(args.in[16] + (size_t)l * FF * DM, FF, DM, DM / 32, (unsigned char*)(ws + WS_WDN + l * SZ_WDN), 128.f, args.in[16], args.in[16], 0, scr, r, lane);
	s_add_u32 s8, s38, 0x3000
	s_addc_u32 s9, s39, 0
	global_load_dwordx4 v[176:179], v75, s[8:9]
	s_add_u32 s8, s8, 0x8000
	s_addc_u32 s9, s9, 0
	global_load_dwordx4 v[180:183], v75, s[8:9]
	s_add_u32 s8, s8, 0x8000
	s_addc_u32 s9, s9, 0
	global_load_dwordx4 v[184:187], v75, s[8:9]
	s_add_u32 s8, s8, 0x8000
	s_addc_u32 s9, s9, 0
	global_load_dwordx4 v[188:191], v75, s[8:9]
	s_add_u32 s8, s8, 0x8000
	s_addc_u32 s9, s9, 0
	global_load_dwordx4 v[192:195], v75, s[8:9]
	s_add_u32 s8, s8, 0x8000
	s_addc_u32 s9, s9, 0
	global_load_dwordx4 v[196:199], v75, s[8:9]
	s_add_u32 s8, s8, 0x8000
	s_addc_u32 s9, s9, 0
	global_load_dwordx4 v[200:203], v75, s[8:9]
	s_add_u32 s8, s8, 0x8000
	s_addc_u32 s9, s9, 0
	global_load_dwordx4 v[204:207], v75, s[8:9]
	s_add_u32 s6, s40, 0x1000000
	s_addc_u32 s7, s41, 0
	ds_read_b32 v226, v212
	ds_read_b32 v227, v212 offset:512
	ds_read_b32 v228, v212 offset:1024
	ds_read_b32 v229, v212 offset:1536
	ds_read_b32 v230, v212 offset:2048
	ds_read_b32 v231, v212 offset:2560
	ds_read_b32 v232, v212 offset:3072
	ds_read_b32 v233, v212 offset:3584
	ds_read_b32 v234, v212 offset:4096
	ds_read_b32 v235, v212 offset:4608
	ds_read_b32 v236, v212 offset:5120
	ds_read_b32 v237, v212 offset:5632
	ds_read_b32 v238, v212 offset:6144
	ds_read_b32 v239, v212 offset:6656
	ds_read_b32 v240, v212 offset:7168
	ds_read_b32 v241, v212 offset:7680
	s_waitcnt lgkmcnt(0)
	v_max_f32_e32 v226, v226, v226
	v_max_f32_e32 v227, v227, v227
	v_max_f32_e32 v228, v228, v228
	v_max_f32_e32 v229, v229, v229
	v_max_f32_e32 v230, v230, v230
	v_max_f32_e32 v231, v231, v231
	v_max_f32_e32 v232, v232, v232
	v_max_f32_e32 v233, v233, v233
	v_max_f32_e32 v234, v234, v234
	v_max_f32_e32 v235, v235, v235
	v_max_f32_e32 v236, v236, v236
	v_max_f32_e32 v237, v237, v237
	v_max_f32_e32 v238, v238, v238
	v_max_f32_e32 v239, v239, v239
	v_max_f32_e32 v240, v240, v240
	v_max_f32_e32 v241, v241, v241
	v_med3_f32 v226, v226, s62, v95
	v_med3_f32 v227, v227, s62, v95
	v_med3_f32 v228, v228, s62, v95
	v_med3_f32 v229, v229, s62, v95
	v_med3_f32 v230, v230, s62, v95
	v_med3_f32 v231, v231, s62, v95
	v_med3_f32 v232, v232, s62, v95
	v_med3_f32 v233, v233, s62, v95
	v_med3_f32 v234, v234, s62, v95
	v_med3_f32 v235, v235, s62, v95
	v_med3_f32 v236, v236, s62, v95
	v_med3_f32 v237, v237, s62, v95
	v_med3_f32 v238, v238, s62, v95
	v_med3_f32 v239, v239, s62, v95
	v_med3_f32 v240, v240, s62, v95
	v_med3_f32 v241, v241, s62, v95
	v_mov_b32_e32 v242, 0
	v_mov_b32_e32 v243, 0
	v_mov_b32_e32 v244, 0
	v_mov_b32_e32 v245, 0
	v_cvt_pk_fp8_f32 v242, v226, v227
	v_cvt_pk_fp8_f32 v243, v230, v231
	v_cvt_pk_fp8_f32 v244, v234, v235
	v_cvt_pk_fp8_f32 v245, v238, v239
	v_cvt_pk_fp8_f32 v242, v228, v229 op_sel:[0,0,1]
	v_cvt_pk_fp8_f32 v243, v232, v233 op_sel:[0,0,1]
	v_cvt_pk_fp8_f32 v244, v236, v237 op_sel:[0,0,1]
	v_cvt_pk_fp8_f32 v245, v240, v241 op_sel:[0,0,1]
	s_nop 0
	global_store_dwordx4 v79, v[242:245], s[6:7]
	ds_read_b32 v226, v214
	ds_read_b32 v227, v214 offset:512
	ds_read_b32 v228, v214 offset:1024
	ds_read_b32 v229, v214 offset:1536
	ds_read_b32 v230, v214 offset:2048
	ds_read_b32 v231, v214 offset:2560
	ds_read_b32 v232, v214 offset:3072
	ds_read_b32 v233, v214 offset:3584
	ds_read_b32 v234, v214 offset:4096
	ds_read_b32 v235, v214 offset:4608
	ds_read_b32 v236, v214 offset:5120
	ds_read_b32 v237, v214 offset:5632
	ds_read_b32 v238, v214 offset:6144
	ds_read_b32 v239, v214 offset:6656
	ds_read_b32 v240, v214 offset:7168
	ds_read_b32 v241, v214 offset:7680
	s_waitcnt lgkmcnt(0)
	v_max_f32_e32 v226, v226, v226
	v_max_f32_e32 v227, v227, v227
	v_max_f32_e32 v228, v228, v228
	v_max_f32_e32 v229, v229, v229
	v_max_f32_e32 v230, v230, v230
	v_max_f32_e32 v231, v231, v231
	v_max_f32_e32 v232, v232, v232
	v_max_f32_e32 v233, v233, v233
	v_max_f32_e32 v234, v234, v234
	v_max_f32_e32 v235, v235, v235
	v_max_f32_e32 v236, v236, v236
	v_max_f32_e32 v237, v237, v237
	v_max_f32_e32 v238, v238, v238
	v_max_f32_e32 v239, v239, v239
	v_max_f32_e32 v240, v240, v240
	v_max_f32_e32 v241, v241, v241
	v_med3_f32 v226, v226, s62, v95
	v_med3_f32 v227, v227, s62, v95
	v_med3_f32 v228, v228, s62, v95
	v_med3_f32 v229, v229, s62, v95
	v_med3_f32 v230, v230, s62, v95
	v_med3_f32 v231, v231, s62, v95
	v_med3_f32 v232, v232, s62, v95
	v_med3_f32 v233, v233, s62, v95
	v_med3_f32 v234, v234, s62, v95
	v_med3_f32 v235, v235, s62, v95
	v_med3_f32 v236, v236, s62, v95
	v_med3_f32 v237, v237, s62, v95
	v_med3_f32 v238, v238, s62, v95
	v_med3_f32 v239, v239, s62, v95
	v_med3_f32 v240, v240, s62, v95
	v_med3_f32 v241, v241, s62, v95
	v_mov_b32_e32 v242, 0
	v_mov_b32_e32 v243, 0
	v_mov_b32_e32 v244, 0
	v_mov_b32_e32 v245, 0
	v_cvt_pk_fp8_f32 v242, v226, v227
	v_cvt_pk_fp8_f32 v243, v230, v231
	v_cvt_pk_fp8_f32 v244, v234, v235
	v_cvt_pk_fp8_f32 v245, v238, v239
	v_cvt_pk_fp8_f32 v242, v228, v229 op_sel:[0,0,1]
	v_cvt_pk_fp8_f32 v243, v232, v233 op_sel:[0,0,1]
	v_cvt_pk_fp8_f32 v244, v236, v237 op_sel:[0,0,1]
	v_cvt_pk_fp8_f32 v245, v240, v241 op_sel:[0,0,1]
	s_nop 0
	global_store_dwordx4 v80, v[242:245], s[6:7]
	s_waitcnt vmcnt(12)
	v_mul_f32_e32 v144, 0x43000000, v144
	v_mul_f32_e32 v145, 0x43000000, v145
	v_mul_f32_e32 v146, 0x43000000, v146
	v_mul_f32_e32 v147, 0x43000000, v147
	ds_write_b128 v209, v[144:147]
	v_mul_f32_e32 v148, 0x43000000, v148
	v_mul_f32_e32 v149, 0x43000000, v149
	v_mul_f32_e32 v150, 0x43000000, v150
	v_mul_f32_e32 v151, 0x43000000, v151
	ds_write_b128 v209, v[148:151] offset:1024
	v_mul_f32_e32 v152, 0x43000000, v152
	v_mul_f32_e32 v153, 0x43000000, v153
	v_mul_f32_e32 v154, 0x43000000, v154
	v_mul_f32_e32 v155, 0x43000000, v155
	ds_write_b128 v209, v[152:155] offset:2048
	v_mul_f32_e32 v156, 0x43000000, v156
	v_mul_f32_e32 v157, 0x43000000, v157
	v_mul_f32_e32 v158, 0x43000000, v158
	v_mul_f32_e32 v159, 0x43000000, v159
	ds_write_b128 v209, v[156:159] offset:3072
	v_mul_f32_e32 v160, 0x43000000, v160
	v_mul_f32_e32 v161, 0x43000000, v161
	v_mul_f32_e32 v162, 0x43000000, v162
	v_mul_f32_e32 v163, 0x43000000, v163
	ds_write_b128 v209, v[160:163] offset:4096
	v_mul_f32_e32 v164, 0x43000000, v164
	v_mul_f32_e32 v165, 0x43000000, v165
	v_mul_f32_e32 v166, 0x43000000, v166
	v_mul_f32_e32 v167, 0x43000000, v167
	ds_write_b128 v209, v[164:167] offset:5120
	v_mul_f32_e32 v168, 0x43000000, v168
	v_mul_f32_e32 v169, 0x43000000, v169
	v_mul_f32_e32 v170, 0x43000000, v170
	v_mul_f32_e32 v171, 0x43000000, v171
	ds_write_b128 v209, v[168:171] offset:6144
	v_mul_f32_e32 v172, 0x43000000, v172
	v_mul_f32_e32 v173, 0x43000000, v173
	v_mul_f32_e32 v174, 0x43000000, v174
	v_mul_f32_e32 v175, 0x43000000, v175
	ds_write_b128 v209, v[172:175] offset:7168
	s_waitcnt lgkmcnt(0)
	s_barrier
; #define GAS __attribute__((address_space(1)))
; #define LAS __attribute__((address_space(3)))
; #define LDS_WAIT() asm volatile("s_waitcnt lgkmcnt(0)" ::: "memory")
;     const int pr = item >> 1, kb = 2 * (pr / nblk) + (item & 1), nb = pr % nblk, k0 = 64 * kb, n0 = 32 * nb;
;     const int nr = n0 + (lane & 31); const int sc = MAP == 1 ? src_col_in(nr) : nr;
;     float v[32];
; #pragma unroll
;     for (int i = 0; i < 32; ++i) v[i] = sc >= 0 ? W[(size_t)(k0 + 2 * i + (lane >> 5)) * Nsrc + sc] : 0.f;
; #pragma unroll
;     for (int i = 0; i < 32; ++i) { const int k = k0 + 2 * i + (lane >> 5); float x = v[i] * wscale; if (KS) x *= (k < ksplit ? ksA[k] : ksB[k - ksplit]); scr[(2 * i + (lane >> 5)) * 33 + (lane & 31)] = x; }
;     LDS_WAIT(); asm volatile("" ::: "memory");
;     const int c = lane & 7;
; #pragma unroll
;     for (int j = 0; j < 4; ++j) { const int n = (lane >> 3) + 8 * j; const LAS float* s = scr + (8 * c) * 33 + n;
;         const unsigned long long o = (unsigned long long)pg8::pk4_fp8(s[0 * 33], s[1 * 33], s[2 * 33], s[3 * 33]) | ((unsigned long long)pg8::pk4_fp8(s[4 * 33], s[5 * 33], s[6 * 33], s[7 * 33]) << 32);
;         *(GAS unsigned long long*)(WT + (size_t)(n0 + n) * K + k0 + 8 * c) = o; }
;     LDS_WAIT(); asm volatile("" ::: "memory");
; }
; __global__ void __launch_bounds__(NWAVES * 64, 2) hybrid_fwd(Args args) {
;     ...
;             p0_transpose_item_f8<false>(args.in[16] + (size_t)l * FF * DM, FF, DM, DM / 32, (unsigned char*)(ws + WS_WDN + l * SZ_WDN), 128.f, args.in[16], args.in[16], 0, scr, r, lane);
	s_add_u32 s8, s38, 0x4000000
	s_addc_u32 s9, s39, 0
	global_load_dwordx4 v[144:147], v75, s[8:9]
	s_add_u32 s8, s8, 0x8000
	s_addc_u32 s9, s9, 0
	global_load_dwordx4 v[148:151], v75, s[8:9]
	s_add_u32 s8, s8, 0x8000
	s_addc_u32 s9, s9, 0
	global_load_dwordx4 v[152:155], v75, s[8:9]
	s_add_u32 s8, s8, 0x8000
	s_addc_u32 s9, s9, 0
	global_load_dwordx4 v[156:159], v75, s[8:9]
	s_add_u32 s8, s8, 0x8000
	s_addc_u32 s9, s9, 0
	global_load_dwordx4 v[160:163], v75, s[8:9]
	s_add_u32 s8, s8, 0x8000
	s_addc_u32 s9, s9, 0
	global_load_dwordx4 v[164:167], v75, s[8:9]
	s_add_u32 s8, s8, 0x8000
	s_addc_u32 s9, s9, 0
	global_load_dwordx4 v[168:171], v75, s[8:9]
	s_add_u32 s8, s8, 0x8000
	s_addc_u32 s9, s9, 0
	global_load_dwordx4 v[172:175], v75, s[8:9]
	s_add_u32 s6, s40, 0x2000000
	s_addc_u32 s7, s41, 0
	ds_read_b32 v226, v211
	ds_read_b32 v227, v211 offset:512
	ds_read_b32 v228, v211 offset:1024
	ds_read_b32 v229, v211 offset:1536
	ds_read_b32 v230, v211 offset:2048
	ds_read_b32 v231, v211 offset:2560
	ds_read_b32 v232, v211 offset:3072
	ds_read_b32 v233, v211 offset:3584
	ds_read_b32 v234, v211 offset:4096
	ds_read_b32 v235, v211 offset:4608
	ds_read_b32 v236, v211 offset:5120
	ds_read_b32 v237, v211 offset:5632
	ds_read_b32 v238, v211 offset:6144
	ds_read_b32 v239, v211 offset:6656
	ds_read_b32 v240, v211 offset:7168
	ds_read_b32 v241, v211 offset:7680
	s_waitcnt lgkmcnt(0)
	v_max_f32_e32 v226, v226, v226
	v_max_f32_e32 v227, v227, v227
	v_max_f32_e32 v228, v228, v228
	v_max_f32_e32 v229, v229, v229
	v_max_f32_e32 v230, v230, v230
	v_max_f32_e32 v231, v231, v231
	v_max_f32_e32 v232, v232, v232
	v_max_f32_e32 v233, v233, v233
	v_max_f32_e32 v234, v234, v234
	v_max_f32_e32 v235, v235, v235
	v_max_f32_e32 v236, v236, v236
	v_max_f32_e32 v237, v237, v237
	v_max_f32_e32 v238, v238, v238
	v_max_f32_e32 v239, v239, v239
	v_max_f32_e32 v240, v240, v240
	v_max_f32_e32 v241, v241, v241
	v_med3_f32 v226, v226, s62, v95
	v_med3_f32 v227, v227, s62, v95
	v_med3_f32 v228, v228, s62, v95
	v_med3_f32 v229, v229, s62, v95
	v_med3_f32 v230, v230, s62, v95
	v_med3_f32 v231, v231, s62, v95
	v_med3_f32 v232, v232, s62, v95
	v_med3_f32 v233, v233, s62, v95
	v_med3_f32 v234, v234, s62, v95
	v_med3_f32 v235, v235, s62, v95
	v_med3_f32 v236, v236, s62, v95
	v_med3_f32 v237, v237, s62, v95
	v_med3_f32 v238, v238, s62, v95
	v_med3_f32 v239, v239, s62, v95
	v_med3_f32 v240, v240, s62, v95
	v_med3_f32 v241, v241, s62, v95
	v_mov_b32_e32 v242, 0
	v_mov_b32_e32 v243, 0
	v_mov_b32_e32 v244, 0
	v_mov_b32_e32 v245, 0
	v_cvt_pk_fp8_f32 v242, v226, v227
	v_cvt_pk_fp8_f32 v243, v230, v231
	v_cvt_pk_fp8_f32 v244, v234, v235
	v_cvt_pk_fp8_f32 v245, v238, v239
	v_cvt_pk_fp8_f32 v242, v228, v229 op_sel:[0,0,1]
	v_cvt_pk_fp8_f32 v243, v232, v233 op_sel:[0,0,1]
	v_cvt_pk_fp8_f32 v244, v236, v237 op_sel:[0,0,1]
	v_cvt_pk_fp8_f32 v245, v240, v241 op_sel:[0,0,1]
	s_nop 0
	global_store_dwordx4 v79, v[242:245], s[6:7]
	ds_read_b32 v226, v213
	ds_read_b32 v227, v213 offset:512
	ds_read_b32 v228, v213 offset:1024
	ds_read_b32 v229, v213 offset:1536
	ds_read_b32 v230, v213 offset:2048
	ds_read_b32 v231, v213 offset:2560
	ds_read_b32 v232, v213 offset:3072
	ds_read_b32 v233, v213 offset:3584
	ds_read_b32 v234, v213 offset:4096
	ds_read_b32 v235, v213 offset:4608
	ds_read_b32 v236, v213 offset:5120
	ds_read_b32 v237, v213 offset:5632
	ds_read_b32 v238, v213 offset:6144
	ds_read_b32 v239, v213 offset:6656
	ds_read_b32 v240, v213 offset:7168
	ds_read_b32 v241, v213 offset:7680
	s_waitcnt lgkmcnt(0)
	v_max_f32_e32 v226, v226, v226
	v_max_f32_e32 v227, v227, v227
	v_max_f32_e32 v228, v228, v228
	v_max_f32_e32 v229, v229, v229
	v_max_f32_e32 v230, v230, v230
	v_max_f32_e32 v231, v231, v231
	v_max_f32_e32 v232, v232, v232
	v_max_f32_e32 v233, v233, v233
	v_max_f32_e32 v234, v234, v234
	v_max_f32_e32 v235, v235, v235
	v_max_f32_e32 v236, v236, v236
	v_max_f32_e32 v237, v237, v237
	v_max_f32_e32 v238, v238, v238
	v_max_f32_e32 v239, v239, v239
	v_max_f32_e32 v240, v240, v240
	v_max_f32_e32 v241, v241, v241
	v_med3_f32 v226, v226, s62, v95
	v_med3_f32 v227, v227, s62, v95
	v_med3_f32 v228, v228, s62, v95
	v_med3_f32 v229, v229, s62, v95
	v_med3_f32 v230, v230, s62, v95
	v_med3_f32 v231, v231, s62, v95
	v_med3_f32 v232, v232, s62, v95
	v_med3_f32 v233, v233, s62, v95
	v_med3_f32 v234, v234, s62, v95
	v_med3_f32 v235, v235, s62, v95
	v_med3_f32 v236, v236, s62, v95
	v_med3_f32 v237, v237, s62, v95
	v_med3_f32 v238, v238, s62, v95
	v_med3_f32 v239, v239, s62, v95
	v_med3_f32 v240, v240, s62, v95
	v_med3_f32 v241, v241, s62, v95
	v_mov_b32_e32 v242, 0
	v_mov_b32_e32 v243, 0
	v_mov_b32_e32 v244, 0
	v_mov_b32_e32 v245, 0
	v_cvt_pk_fp8_f32 v242, v226, v227
	v_cvt_pk_fp8_f32 v243, v230, v231
	v_cvt_pk_fp8_f32 v244, v234, v235
	v_cvt_pk_fp8_f32 v245, v238, v239
	v_cvt_pk_fp8_f32 v242, v228, v229 op_sel:[0,0,1]
	v_cvt_pk_fp8_f32 v243, v232, v233 op_sel:[0,0,1]
	v_cvt_pk_fp8_f32 v244, v236, v237 op_sel:[0,0,1]
	v_cvt_pk_fp8_f32 v245, v240, v241 op_sel:[0,0,1]
	s_nop 0
	global_store_dwordx4 v80, v[242:245], s[6:7]
	s_waitcnt vmcnt(12)
	v_mul_f32_e32 v176, 0x43000000, v176
	v_mul_f32_e32 v177, 0x43000000, v177
	v_mul_f32_e32 v178, 0x43000000, v178
	v_mul_f32_e32 v179, 0x43000000, v179
	ds_write_b128 v210, v[176:179]
	v_mul_f32_e32 v180, 0x43000000, v180
	v_mul_f32_e32 v181, 0x43000000, v181
	v_mul_f32_e32 v182, 0x43000000, v182
	v_mul_f32_e32 v183, 0x43000000, v183
	ds_write_b128 v210, v[180:183] offset:1024
	v_mul_f32_e32 v184, 0x43000000, v184
	v_mul_f32_e32 v185, 0x43000000, v185
	v_mul_f32_e32 v186, 0x43000000, v186
	v_mul_f32_e32 v187, 0x43000000, v187
	ds_write_b128 v210, v[184:187] offset:2048
	v_mul_f32_e32 v188, 0x43000000, v188
	v_mul_f32_e32 v189, 0x43000000, v189
	v_mul_f32_e32 v190, 0x43000000, v190
	v_mul_f32_e32 v191, 0x43000000, v191
	ds_write_b128 v210, v[188:191] offset:3072
	v_mul_f32_e32 v192, 0x43000000, v192
	v_mul_f32_e32 v193, 0x43000000, v193
	v_mul_f32_e32 v194, 0x43000000, v194
	v_mul_f32_e32 v195, 0x43000000, v195
	ds_write_b128 v210, v[192:195] offset:4096
	v_mul_f32_e32 v196, 0x43000000, v196
	v_mul_f32_e32 v197, 0x43000000, v197
	v_mul_f32_e32 v198, 0x43000000, v198
	v_mul_f32_e32 v199, 0x43000000, v199
	ds_write_b128 v210, v[196:199] offset:5120
	v_mul_f32_e32 v200, 0x43000000, v200
	v_mul_f32_e32 v201, 0x43000000, v201
	v_mul_f32_e32 v202, 0x43000000, v202
	v_mul_f32_e32 v203, 0x43000000, v203
	ds_write_b128 v210, v[200:203] offset:6144
	v_mul_f32_e32 v204, 0x43000000, v204
	v_mul_f32_e32 v205, 0x43000000, v205
	v_mul_f32_e32 v206, 0x43000000, v206
	v_mul_f32_e32 v207, 0x43000000, v207
	ds_write_b128 v210, v[204:207] offset:7168
	s_waitcnt lgkmcnt(0)
	s_barrier
; #define GAS __attribute__((address_space(1)))
; #define LAS __attribute__((address_space(3)))
; #define LDS_WAIT() asm volatile("s_waitcnt lgkmcnt(0)" ::: "memory")
;     const int pr = item >> 1, kb = 2 * (pr / nblk) + (item & 1), nb = pr % nblk, k0 = 64 * kb, n0 = 32 * nb;
;     const int nr = n0 + (lane & 31); const int sc = MAP == 1 ? src_col_in(nr) : nr;
;     float v[32];
; #pragma unroll
;     for (int i = 0; i < 32; ++i) v[i] = sc >= 0 ? W[(size_t)(k0 + 2 * i + (lane >> 5)) * Nsrc + sc] : 0.f;
; #pragma unroll
;     for (int i = 0; i < 32; ++i) { const int k = k0 + 2 * i + (lane >> 5); float x = v[i] * wscale; if (KS) x *= (k < ksplit ? ksA[k] : ksB[k - ksplit]); scr[(2 * i + (lane >> 5)) * 33 + (lane & 31)] = x; }
;     LDS_WAIT(); asm volatile("" ::: "memory");
;     const int c = lane & 7;
; #pragma unroll
;     for (int j = 0; j < 4; ++j) { const int n = (lane >> 3) + 8 * j; const LAS float* s = scr + (8 * c) * 33 + n;
;         const unsigned long long o = (unsigned long long)pg8::pk4_fp8(s[0 * 33], s[1 * 33], s[2 * 33], s[3 * 33]) | ((unsigned long long)pg8::pk4_fp8(s[4 * 33], s[5 * 33], s[6 * 33], s[7 * 33]) << 32);
;         *(GAS unsigned long long*)(WT + (size_t)(n0 + n) * K + k0 + 8 * c) = o; }
;     LDS_WAIT(); asm volatile("" ::: "memory");
; }
; __global__ void __launch_bounds__(NWAVES * 64, 2) hybrid_fwd(Args args) {
;     ...
;             p0_transpose_item_f8<false>(args.in[16] + (size_t)l * FF * DM, FF, DM, DM / 32, (unsigned char*)(ws + WS_WDN + l * SZ_WDN), 128.f, args.in[16], args.in[16], 0, scr, r, lane);
	s_add_u32 s8, s38, 0x4001000
	s_addc_u32 s9, s39, 0
	global_load_dwordx4 v[176:179], v75, s[8:9]
	s_add_u32 s8, s8, 0x8000
	s_addc_u32 s9, s9, 0
	global_load_dwordx4 v[180:183], v75, s[8:9]
	s_add_u32 s8, s8, 0x8000
	s_addc_u32 s9, s9, 0
	global_load_dwordx4 v[184:187], v75, s[8:9]
	s_add_u32 s8, s8, 0x8000
	s_addc_u32 s9, s9, 0
	global_load_dwordx4 v[188:191], v75, s[8:9]
	s_add_u32 s8, s8, 0x8000
	s_addc_u32 s9, s9, 0
	global_load_dwordx4 v[192:195], v75, s[8:9]
	s_add_u32 s8, s8, 0x8000
	s_addc_u32 s9, s9, 0
	global_load_dwordx4 v[196:199], v75, s[8:9]
	s_add_u32 s8, s8, 0x8000
	s_addc_u32 s9, s9, 0
	global_load_dwordx4 v[200:203], v75, s[8:9]
	s_add_u32 s8, s8, 0x8000
	s_addc_u32 s9, s9, 0
	global_load_dwordx4 v[204:207], v75, s[8:9]
	s_add_u32 s6, s40, 0x3000000
	s_addc_u32 s7, s41, 0
	ds_read_b32 v226, v212
	ds_read_b32 v227, v212 offset:512
	ds_read_b32 v228, v212 offset:1024
	ds_read_b32 v229, v212 offset:1536
	ds_read_b32 v230, v212 offset:2048
	ds_read_b32 v231, v212 offset:2560
	ds_read_b32 v232, v212 offset:3072
	ds_read_b32 v233, v212 offset:3584
	ds_read_b32 v234, v212 offset:4096
	ds_read_b32 v235, v212 offset:4608
	ds_read_b32 v236, v212 offset:5120
	ds_read_b32 v237, v212 offset:5632
	ds_read_b32 v238, v212 offset:6144
	ds_read_b32 v239, v212 offset:6656
	ds_read_b32 v240, v212 offset:7168
	ds_read_b32 v241, v212 offset:7680
	s_waitcnt lgkmcnt(0)
	v_max_f32_e32 v226, v226, v226
	v_max_f32_e32 v227, v227, v227
	v_max_f32_e32 v228, v228, v228
	v_max_f32_e32 v229, v229, v229
	v_max_f32_e32 v230, v230, v230
	v_max_f32_e32 v231, v231, v231
	v_max_f32_e32 v232, v232, v232
	v_max_f32_e32 v233, v233, v233
	v_max_f32_e32 v234, v234, v234
	v_max_f32_e32 v235, v235, v235
	v_max_f32_e32 v236, v236, v236
	v_max_f32_e32 v237, v237, v237
	v_max_f32_e32 v238, v238, v238
	v_max_f32_e32 v239, v239, v239
	v_max_f32_e32 v240, v240, v240
	v_max_f32_e32 v241, v241, v241
	v_med3_f32 v226, v226, s62, v95
	v_med3_f32 v227, v227, s62, v95
	v_med3_f32 v228, v228, s62, v95
	v_med3_f32 v229, v229, s62, v95
	v_med3_f32 v230, v230, s62, v95
	v_med3_f32 v231, v231, s62, v95
	v_med3_f32 v232, v232, s62, v95
	v_med3_f32 v233, v233, s62, v95
	v_med3_f32 v234, v234, s62, v95
	v_med3_f32 v235, v235, s62, v95
	v_med3_f32 v236, v236, s62, v95
	v_med3_f32 v237, v237, s62, v95
	v_med3_f32 v238, v238, s62, v95
	v_med3_f32 v239, v239, s62, v95
	v_med3_f32 v240, v240, s62, v95
	v_med3_f32 v241, v241, s62, v95
	v_mov_b32_e32 v242, 0
	v_mov_b32_e32 v243, 0
	v_mov_b32_e32 v244, 0
	v_mov_b32_e32 v245, 0
	v_cvt_pk_fp8_f32 v242, v226, v227
	v_cvt_pk_fp8_f32 v243, v230, v231
	v_cvt_pk_fp8_f32 v244, v234, v235
	v_cvt_pk_fp8_f32 v245, v238, v239
	v_cvt_pk_fp8_f32 v242, v228, v229 op_sel:[0,0,1]
	v_cvt_pk_fp8_f32 v243, v232, v233 op_sel:[0,0,1]
	v_cvt_pk_fp8_f32 v244, v236, v237 op_sel:[0,0,1]
	v_cvt_pk_fp8_f32 v245, v240, v241 op_sel:[0,0,1]
	s_nop 0
	global_store_dwordx4 v79, v[242:245], s[6:7]
	ds_read_b32 v226, v214
	ds_read_b32 v227, v214 offset:512
	ds_read_b32 v228, v214 offset:1024
	ds_read_b32 v229, v214 offset:1536
	ds_read_b32 v230, v214 offset:2048
	ds_read_b32 v231, v214 offset:2560
	ds_read_b32 v232, v214 offset:3072
	ds_read_b32 v233, v214 offset:3584
	ds_read_b32 v234, v214 offset:4096
	ds_read_b32 v235, v214 offset:4608
	ds_read_b32 v236, v214 offset:5120
	ds_read_b32 v237, v214 offset:5632
	ds_read_b32 v238, v214 offset:6144
	ds_read_b32 v239, v214 offset:6656
	ds_read_b32 v240, v214 offset:7168
	ds_read_b32 v241, v214 offset:7680
	s_waitcnt lgkmcnt(0)
	v_max_f32_e32 v226, v226, v226
	v_max_f32_e32 v227, v227, v227
	v_max_f32_e32 v228, v228, v228
	v_max_f32_e32 v229, v229, v229
	v_max_f32_e32 v230, v230, v230
	v_max_f32_e32 v231, v231, v231
	v_max_f32_e32 v232, v232, v232
	v_max_f32_e32 v233, v233, v233
	v_max_f32_e32 v234, v234, v234
	v_max_f32_e32 v235, v235, v235
	v_max_f32_e32 v236, v236, v236
	v_max_f32_e32 v237, v237, v237
	v_max_f32_e32 v238, v238, v238
	v_max_f32_e32 v239, v239, v239
	v_max_f32_e32 v240, v240, v240
	v_max_f32_e32 v241, v241, v241
	v_med3_f32 v226, v226, s62, v95
	v_med3_f32 v227, v227, s62, v95
	v_med3_f32 v228, v228, s62, v95
	v_med3_f32 v229, v229, s62, v95
	v_med3_f32 v230, v230, s62, v95
	v_med3_f32 v231, v231, s62, v95
	v_med3_f32 v232, v232, s62, v95
	v_med3_f32 v233, v233, s62, v95
	v_med3_f32 v234, v234, s62, v95
	v_med3_f32 v235, v235, s62, v95
	v_med3_f32 v236, v236, s62, v95
	v_med3_f32 v237, v237, s62, v95
	v_med3_f32 v238, v238, s62, v95
	v_med3_f32 v239, v239, s62, v95
	v_med3_f32 v240, v240, s62, v95
	v_med3_f32 v241, v241, s62, v95
	v_mov_b32_e32 v242, 0
	v_mov_b32_e32 v243, 0
	v_mov_b32_e32 v244, 0
	v_mov_b32_e32 v245, 0
	v_cvt_pk_fp8_f32 v242, v226, v227
	v_cvt_pk_fp8_f32 v243, v230, v231
	v_cvt_pk_fp8_f32 v244, v234, v235
	v_cvt_pk_fp8_f32 v245, v238, v239
	v_cvt_pk_fp8_f32 v242, v228, v229 op_sel:[0,0,1]
	v_cvt_pk_fp8_f32 v243, v232, v233 op_sel:[0,0,1]
	v_cvt_pk_fp8_f32 v244, v236, v237 op_sel:[0,0,1]
	v_cvt_pk_fp8_f32 v245, v240, v241 op_sel:[0,0,1]
	s_nop 0
	global_store_dwordx4 v80, v[242:245], s[6:7]
	s_waitcnt vmcnt(12)
	v_mul_f32_e32 v144, 0x43000000, v144
	v_mul_f32_e32 v145, 0x43000000, v145
	v_mul_f32_e32 v146, 0x43000000, v146
	v_mul_f32_e32 v147, 0x43000000, v147
	ds_write_b128 v209, v[144:147]
	v_mul_f32_e32 v148, 0x43000000, v148
	v_mul_f32_e32 v149, 0x43000000, v149
	v_mul_f32_e32 v150, 0x43000000, v150
	v_mul_f32_e32 v151, 0x43000000, v151
	ds_write_b128 v209, v[148:151] offset:1024
	v_mul_f32_e32 v152, 0x43000000, v152
	v_mul_f32_e32 v153, 0x43000000, v153
	v_mul_f32_e32 v154, 0x43000000, v154
	v_mul_f32_e32 v155, 0x43000000, v155
	ds_write_b128 v209, v[152:155] offset:2048
	v_mul_f32_e32 v156, 0x43000000, v156
	v_mul_f32_e32 v157, 0x43000000, v157
	v_mul_f32_e32 v158, 0x43000000, v158
	v_mul_f32_e32 v159, 0x43000000, v159
	ds_write_b128 v209, v[156:159] offset:3072
	v_mul_f32_e32 v160, 0x43000000, v160
	v_mul_f32_e32 v161, 0x43000000, v161
	v_mul_f32_e32 v162, 0x43000000, v162
	v_mul_f32_e32 v163, 0x43000000, v163
	ds_write_b128 v209, v[160:163] offset:4096
	v_mul_f32_e32 v164, 0x43000000, v164
	v_mul_f32_e32 v165, 0x43000000, v165
	v_mul_f32_e32 v166, 0x43000000, v166
	v_mul_f32_e32 v167, 0x43000000, v167
	ds_write_b128 v209, v[164:167] offset:5120
	v_mul_f32_e32 v168, 0x43000000, v168
	v_mul_f32_e32 v169, 0x43000000, v169
	v_mul_f32_e32 v170, 0x43000000, v170
	v_mul_f32_e32 v171, 0x43000000, v171
	ds_write_b128 v209, v[168:171] offset:6144
	v_mul_f32_e32 v172, 0x43000000, v172
	v_mul_f32_e32 v173, 0x43000000, v173
	v_mul_f32_e32 v174, 0x43000000, v174
	v_mul_f32_e32 v175, 0x43000000, v175
	ds_write_b128 v209, v[172:175] offset:7168
	s_waitcnt lgkmcnt(0)
	s_barrier
; #define GAS __attribute__((address_space(1)))
; #define LAS __attribute__((address_space(3)))
; #define LDS_WAIT() asm volatile("s_waitcnt lgkmcnt(0)" ::: "memory")
;     const int pr = item >> 1, kb = 2 * (pr / nblk) + (item & 1), nb = pr % nblk, k0 = 64 * kb, n0 = 32 * nb;
;     const int nr = n0 + (lane & 31); const int sc = MAP == 1 ? src_col_in(nr) : nr;
;     float v[32];
; #pragma unroll
;     for (int i = 0; i < 32; ++i) v[i] = sc >= 0 ? W[(size_t)(k0 + 2 * i + (lane >> 5)) * Nsrc + sc] : 0.f;
; #pragma unroll
;     for (int i = 0; i < 32; ++i) { const int k = k0 + 2 * i + (lane >> 5); float x = v[i] * wscale; if (KS) x *= (k < ksplit ? ksA[k] : ksB[k - ksplit]); scr[(2 * i + (lane >> 5)) * 33 + (lane & 31)] = x; }
;     LDS_WAIT(); asm volatile("" ::: "memory");
;     const int c = lane & 7;
; #pragma unroll
;     for (int j = 0; j < 4; ++j) { const int n = (lane >> 3) + 8 * j; const LAS float* s = scr + (8 * c) * 33 + n;
;         const unsigned long long o = (unsigned long long)pg8::pk4_fp8(s[0 * 33], s[1 * 33], s[2 * 33], s[3 * 33]) | ((unsigned long long)pg8::pk4_fp8(s[4 * 33], s[5 * 33], s[6 * 33], s[7 * 33]) << 32);
;         *(GAS unsigned long long*)(WT + (size_t)(n0 + n) * K + k0 + 8 * c) = o; }
;     LDS_WAIT(); asm volatile("" ::: "memory");
; }
; __global__ void __launch_bounds__(NWAVES * 64, 2) hybrid_fwd(Args args) {
;     ...
;             p0_transpose_item_f8<false>(args.in[16] + (size_t)l * FF * DM, FF, DM, DM / 32, (unsigned char*)(ws + WS_WDN + l * SZ_WDN), 128.f, args.in[16], args.in[16], 0, scr, r, lane);
	s_add_u32 s8, s38, 0x4002000
	s_addc_u32 s9, s39, 0
	global_load_dwordx4 v[144:147], v75, s[8:9]
	s_add_u32 s8, s8, 0x8000
	s_addc_u32 s9, s9, 0
	global_load_dwordx4 v[148:151], v75, s[8:9]
	s_add_u32 s8, s8, 0x8000
	s_addc_u32 s9, s9, 0
	global_load_dwordx4 v[152:155], v75, s[8:9]
	s_add_u32 s8, s8, 0x8000
	s_addc_u32 s9, s9, 0
	global_load_dwordx4 v[156:159], v75, s[8:9]
	s_add_u32 s8, s8, 0x8000
	s_addc_u32 s9, s9, 0
	global_load_dwordx4 v[160:163], v75, s[8:9]
	s_add_u32 s8, s8, 0x8000
	s_addc_u32 s9, s9, 0
	global_load_dwordx4 v[164:167], v75, s[8:9]
	s_add_u32 s8, s8, 0x8000
	s_addc_u32 s9, s9, 0
	global_load_dwordx4 v[168:171], v75, s[8:9]
	s_add_u32 s8, s8, 0x8000
	s_addc_u32 s9, s9, 0
	global_load_dwordx4 v[172:175], v75, s[8:9]
	s_add_u32 s6, s40, 0x1000
	s_addc_u32 s7, s41, 0
	ds_read_b32 v226, v211
	ds_read_b32 v227, v211 offset:512
	ds_read_b32 v228, v211 offset:1024
	ds_read_b32 v229, v211 offset:1536
	ds_read_b32 v230, v211 offset:2048
	ds_read_b32 v231, v211 offset:2560
	ds_read_b32 v232, v211 offset:3072
	ds_read_b32 v233, v211 offset:3584
	ds_read_b32 v234, v211 offset:4096
	ds_read_b32 v235, v211 offset:4608
	ds_read_b32 v236, v211 offset:5120
	ds_read_b32 v237, v211 offset:5632
	ds_read_b32 v238, v211 offset:6144
	ds_read_b32 v239, v211 offset:6656
	ds_read_b32 v240, v211 offset:7168
	ds_read_b32 v241, v211 offset:7680
	s_waitcnt lgkmcnt(0)
	v_max_f32_e32 v226, v226, v226
	v_max_f32_e32 v227, v227, v227
	v_max_f32_e32 v228, v228, v228
	v_max_f32_e32 v229, v229, v229
	v_max_f32_e32 v230, v230, v230
	v_max_f32_e32 v231, v231, v231
	v_max_f32_e32 v232, v232, v232
	v_max_f32_e32 v233, v233, v233
	v_max_f32_e32 v234, v234, v234
	v_max_f32_e32 v235, v235, v235
	v_max_f32_e32 v236, v236, v236
	v_max_f32_e32 v237, v237, v237
	v_max_f32_e32 v238, v238, v238
	v_max_f32_e32 v239, v239, v239
	v_max_f32_e32 v240, v240, v240
	v_max_f32_e32 v241, v241, v241
	v_med3_f32 v226, v226, s62, v95
	v_med3_f32 v227, v227, s62, v95
	v_med3_f32 v228, v228, s62, v95
	v_med3_f32 v229, v229, s62, v95
	v_med3_f32 v230, v230, s62, v95
	v_med3_f32 v231, v231, s62, v95
	v_med3_f32 v232, v232, s62, v95
	v_med3_f32 v233, v233, s62, v95
	v_med3_f32 v234, v234, s62, v95
	v_med3_f32 v235, v235, s62, v95
	v_med3_f32 v236, v236, s62, v95
	v_med3_f32 v237, v237, s62, v95
	v_med3_f32 v238, v238, s62, v95
	v_med3_f32 v239, v239, s62, v95
	v_med3_f32 v240, v240, s62, v95
	v_med3_f32 v241, v241, s62, v95
	v_mov_b32_e32 v242, 0
	v_mov_b32_e32 v243, 0
	v_mov_b32_e32 v244, 0
	v_mov_b32_e32 v245, 0
	v_cvt_pk_fp8_f32 v242, v226, v227
	v_cvt_pk_fp8_f32 v243, v230, v231
	v_cvt_pk_fp8_f32 v244, v234, v235
	v_cvt_pk_fp8_f32 v245, v238, v239
	v_cvt_pk_fp8_f32 v242, v228, v229 op_sel:[0,0,1]
	v_cvt_pk_fp8_f32 v243, v232, v233 op_sel:[0,0,1]
	v_cvt_pk_fp8_f32 v244, v236, v237 op_sel:[0,0,1]
	v_cvt_pk_fp8_f32 v245, v240, v241 op_sel:[0,0,1]
	s_nop 0
	global_store_dwordx4 v79, v[242:245], s[6:7]
	ds_read_b32 v226, v213
	ds_read_b32 v227, v213 offset:512
	ds_read_b32 v228, v213 offset:1024
	ds_read_b32 v229, v213 offset:1536
	ds_read_b32 v230, v213 offset:2048
	ds_read_b32 v231, v213 offset:2560
	ds_read_b32 v232, v213 offset:3072
	ds_read_b32 v233, v213 offset:3584
	ds_read_b32 v234, v213 offset:4096
	ds_read_b32 v235, v213 offset:4608
	ds_read_b32 v236, v213 offset:5120
	ds_read_b32 v237, v213 offset:5632
	ds_read_b32 v238, v213 offset:6144
	ds_read_b32 v239, v213 offset:6656
	ds_read_b32 v240, v213 offset:7168
	ds_read_b32 v241, v213 offset:7680
	s_waitcnt lgkmcnt(0)
	v_max_f32_e32 v226, v226, v226
	v_max_f32_e32 v227, v227, v227
	v_max_f32_e32 v228, v228, v228
	v_max_f32_e32 v229, v229, v229
	v_max_f32_e32 v230, v230, v230
	v_max_f32_e32 v231, v231, v231
	v_max_f32_e32 v232, v232, v232
	v_max_f32_e32 v233, v233, v233
	v_max_f32_e32 v234, v234, v234
	v_max_f32_e32 v235, v235, v235
	v_max_f32_e32 v236, v236, v236
	v_max_f32_e32 v237, v237, v237
	v_max_f32_e32 v238, v238, v238
	v_max_f32_e32 v239, v239, v239
	v_max_f32_e32 v240, v240, v240
	v_max_f32_e32 v241, v241, v241
	v_med3_f32 v226, v226, s62, v95
	v_med3_f32 v227, v227, s62, v95
	v_med3_f32 v228, v228, s62, v95
	v_med3_f32 v229, v229, s62, v95
	v_med3_f32 v230, v230, s62, v95
	v_med3_f32 v231, v231, s62, v95
	v_med3_f32 v232, v232, s62, v95
	v_med3_f32 v233, v233, s62, v95
	v_med3_f32 v234, v234, s62, v95
	v_med3_f32 v235, v235, s62, v95
	v_med3_f32 v236, v236, s62, v95
	v_med3_f32 v237, v237, s62, v95
	v_med3_f32 v238, v238, s62, v95
	v_med3_f32 v239, v239, s62, v95
	v_med3_f32 v240, v240, s62, v95
	v_med3_f32 v241, v241, s62, v95
	v_mov_b32_e32 v242, 0
	v_mov_b32_e32 v243, 0
	v_mov_b32_e32 v244, 0
	v_mov_b32_e32 v245, 0
	v_cvt_pk_fp8_f32 v242, v226, v227
	v_cvt_pk_fp8_f32 v243, v230, v231
	v_cvt_pk_fp8_f32 v244, v234, v235
	v_cvt_pk_fp8_f32 v245, v238, v239
	v_cvt_pk_fp8_f32 v242, v228, v229 op_sel:[0,0,1]
	v_cvt_pk_fp8_f32 v243, v232, v233 op_sel:[0,0,1]
	v_cvt_pk_fp8_f32 v244, v236, v237 op_sel:[0,0,1]
	v_cvt_pk_fp8_f32 v245, v240, v241 op_sel:[0,0,1]
	s_nop 0
	global_store_dwordx4 v80, v[242:245], s[6:7]
	s_branch .Lco3_hop_skip

; #define GAS __attribute__((address_space(1)))
; #define LAS __attribute__((address_space(3)))
; #define LDS_WAIT() asm volatile("s_waitcnt lgkmcnt(0)" ::: "memory")
;     const int pr = item >> 1, kb = 2 * (pr / nblk) + (item & 1), nb = pr % nblk, k0 = 64 * kb, n0 = 32 * nb;
;     const int nr = n0 + (lane & 31); const int sc = MAP == 1 ? src_col_in(nr) : nr;
;     float v[32];
; #pragma unroll
;     for (int i = 0; i < 32; ++i) v[i] = sc >= 0 ? W[(size_t)(k0 + 2 * i + (lane >> 5)) * Nsrc + sc] : 0.f;
; #pragma unroll
;     for (int i = 0; i < 32; ++i) { const int k = k0 + 2 * i + (lane >> 5); float x = v[i] * wscale; if (KS) x *= (k < ksplit ? ksA[k] : ksB[k - ksplit]); scr[(2 * i + (lane >> 5)) * 33 + (lane & 31)] = x; }
;     LDS_WAIT(); asm volatile("" ::: "memory");
;     const int c = lane & 7;
; #pragma unroll
;     for (int j = 0; j < 4; ++j) { const int n = (lane >> 3) + 8 * j; const LAS float* s = scr + (8 * c) * 33 + n;
;         const unsigned long long o = (unsigned long long)pg8::pk4_fp8(s[0 * 33], s[1 * 33], s[2 * 33], s[3 * 33]) | ((unsigned long long)pg8::pk4_fp8(s[4 * 33], s[5 * 33], s[6 * 33], s[7 * 33]) << 32);
;         *(GAS unsigned long long*)(WT + (size_t)(n0 + n) * K + k0 + 8 * c) = o; }
;     LDS_WAIT(); asm volatile("" ::: "memory");
; }
; __global__ void __launch_bounds__(NWAVES * 64, 2) hybrid_fwd(Args args) {
;     ...
;             p0_transpose_item_f8<false>(args.in[16] + (size_t)l * FF * DM, FF, DM, DM / 32, (unsigned char*)(ws + WS_WDN + l * SZ_WDN), 128.f, args.in[16], args.in[16], 0, scr, r, lane);
.Lco3_hop_skip:
	s_waitcnt vmcnt(12)
	v_mul_f32_e32 v176, 0x43000000, v176
	v_mul_f32_e32 v177, 0x43000000, v177
	v_mul_f32_e32 v178, 0x43000000, v178
	v_mul_f32_e32 v179, 0x43000000, v179
	ds_write_b128 v210, v[176:179]
	v_mul_f32_e32 v180, 0x43000000, v180
	v_mul_f32_e32 v181, 0x43000000, v181
	v_mul_f32_e32 v182, 0x43000000, v182
	v_mul_f32_e32 v183, 0x43000000, v183
	ds_write_b128 v210, v[180:183] offset:1024
	v_mul_f32_e32 v184, 0x43000000, v184
	v_mul_f32_e32 v185, 0x43000000, v185
	v_mul_f32_e32 v186, 0x43000000, v186
	v_mul_f32_e32 v187, 0x43000000, v187
	ds_write_b128 v210, v[184:187] offset:2048
	v_mul_f32_e32 v188, 0x43000000, v188
	v_mul_f32_e32 v189, 0x43000000, v189
	v_mul_f32_e32 v190, 0x43000000, v190
	v_mul_f32_e32 v191, 0x43000000, v191
	ds_write_b128 v210, v[188:191] offset:3072
	v_mul_f32_e32 v192, 0x43000000, v192
	v_mul_f32_e32 v193, 0x43000000, v193
	v_mul_f32_e32 v194, 0x43000000, v194
	v_mul_f32_e32 v195, 0x43000000, v195
	ds_write_b128 v210, v[192:195] offset:4096
	v_mul_f32_e32 v196, 0x43000000, v196
	v_mul_f32_e32 v197, 0x43000000, v197
	v_mul_f32_e32 v198, 0x43000000, v198
	v_mul_f32_e32 v199, 0x43000000, v199
	ds_write_b128 v210, v[196:199] offset:5120
	v_mul_f32_e32 v200, 0x43000000, v200
	v_mul_f32_e32 v201, 0x43000000, v201
	v_mul_f32_e32 v202, 0x43000000, v202
	v_mul_f32_e32 v203, 0x43000000, v203
	ds_write_b128 v210, v[200:203] offset:6144
	v_mul_f32_e32 v204, 0x43000000, v204
	v_mul_f32_e32 v205, 0x43000000, v205
	v_mul_f32_e32 v206, 0x43000000, v206
	v_mul_f32_e32 v207, 0x43000000, v207
	ds_write_b128 v210, v[204:207] offset:7168
	s_waitcnt lgkmcnt(0)
	s_barrier
	s_add_u32 s8, s38, 0x4003000
	s_addc_u32 s9, s39, 0
	global_load_dwordx4 v[176:179], v75, s[8:9]
	s_add_u32 s8, s8, 0x8000
	s_addc_u32 s9, s9, 0
	global_load_dwordx4 v[180:183], v75, s[8:9]
	s_add_u32 s8, s8, 0x8000
	s_addc_u32 s9, s9, 0
	global_load_dwordx4 v[184:187], v75, s[8:9]
	s_add_u32 s8, s8, 0x8000
	s_addc_u32 s9, s9, 0
	global_load_dwordx4 v[188:191], v75, s[8:9]
	s_add_u32 s8, s8, 0x8000
	s_addc_u32 s9, s9, 0
	global_load_dwordx4 v[192:195], v75, s[8:9]
	s_add_u32 s8, s8, 0x8000
	s_addc_u32 s9, s9, 0
	global_load_dwordx4 v[196:199], v75, s[8:9]
	s_add_u32 s8, s8, 0x8000
	s_addc_u32 s9, s9, 0
	global_load_dwordx4 v[200:203], v75, s[8:9]
	s_add_u32 s8, s8, 0x8000
	s_addc_u32 s9, s9, 0
	global_load_dwordx4 v[204:207], v75, s[8:9]
	s_add_u32 s6, s40, 0x1001000
	s_addc_u32 s7, s41, 0
	ds_read_b32 v226, v212
	ds_read_b32 v227, v212 offset:512
	ds_read_b32 v228, v212 offset:1024
	ds_read_b32 v229, v212 offset:1536
	ds_read_b32 v230, v212 offset:2048
	ds_read_b32 v231, v212 offset:2560
	ds_read_b32 v232, v212 offset:3072
	ds_read_b32 v233, v212 offset:3584
	ds_read_b32 v234, v212 offset:4096
	ds_read_b32 v235, v212 offset:4608
	ds_read_b32 v236, v212 offset:5120
	ds_read_b32 v237, v212 offset:5632
	ds_read_b32 v238, v212 offset:6144
	ds_read_b32 v239, v212 offset:6656
	ds_read_b32 v240, v212 offset:7168
	ds_read_b32 v241, v212 offset:7680
	s_waitcnt lgkmcnt(0)
	v_max_f32_e32 v226, v226, v226
	v_max_f32_e32 v227, v227, v227
	v_max_f32_e32 v228, v228, v228
	v_max_f32_e32 v229, v229, v229
	v_max_f32_e32 v230, v230, v230
	v_max_f32_e32 v231, v231, v231
	v_max_f32_e32 v232, v232, v232
	v_max_f32_e32 v233, v233, v233
	v_max_f32_e32 v234, v234, v234
	v_max_f32_e32 v235, v235, v235
	v_max_f32_e32 v236, v236, v236
	v_max_f32_e32 v237, v237, v237
	v_max_f32_e32 v238, v238, v238
	v_max_f32_e32 v239, v239, v239
	v_max_f32_e32 v240, v240, v240
	v_max_f32_e32 v241, v241, v241
	v_med3_f32 v226, v226, s62, v95
	v_med3_f32 v227, v227, s62, v95
	v_med3_f32 v228, v228, s62, v95
	v_med3_f32 v229, v229, s62, v95
	v_med3_f32 v230, v230, s62, v95
	v_med3_f32 v231, v231, s62, v95
	v_med3_f32 v232, v232, s62, v95
	v_med3_f32 v233, v233, s62, v95
	v_med3_f32 v234, v234, s62, v95
	v_med3_f32 v235, v235, s62, v95
	v_med3_f32 v236, v236, s62, v95
	v_med3_f32 v237, v237, s62, v95
	v_med3_f32 v238, v238, s62, v95
	v_med3_f32 v239, v239, s62, v95
	v_med3_f32 v240, v240, s62, v95
	v_med3_f32 v241, v241, s62, v95
	v_mov_b32_e32 v242, 0
	v_mov_b32_e32 v243, 0
	v_mov_b32_e32 v244, 0
	v_mov_b32_e32 v245, 0
	v_cvt_pk_fp8_f32 v242, v226, v227
	v_cvt_pk_fp8_f32 v243, v230, v231
	v_cvt_pk_fp8_f32 v244, v234, v235
	v_cvt_pk_fp8_f32 v245, v238, v239
	v_cvt_pk_fp8_f32 v242, v228, v229 op_sel:[0,0,1]
	v_cvt_pk_fp8_f32 v243, v232, v233 op_sel:[0,0,1]
	v_cvt_pk_fp8_f32 v244, v236, v237 op_sel:[0,0,1]
	v_cvt_pk_fp8_f32 v245, v240, v241 op_sel:[0,0,1]
	s_nop 0
	global_store_dwordx4 v79, v[242:245], s[6:7]
	ds_read_b32 v226, v214
	ds_read_b32 v227, v214 offset:512
	ds_read_b32 v228, v214 offset:1024
	ds_read_b32 v229, v214 offset:1536
	ds_read_b32 v230, v214 offset:2048
	ds_read_b32 v231, v214 offset:2560
	ds_read_b32 v232, v214 offset:3072
	ds_read_b32 v233, v214 offset:3584
	ds_read_b32 v234, v214 offset:4096
	ds_read_b32 v235, v214 offset:4608
	ds_read_b32 v236, v214 offset:5120
	ds_read_b32 v237, v214 offset:5632
	ds_read_b32 v238, v214 offset:6144
	ds_read_b32 v239, v214 offset:6656
	ds_read_b32 v240, v214 offset:7168
	ds_read_b32 v241, v214 offset:7680
	s_waitcnt lgkmcnt(0)
; #define GAS __attribute__((address_space(1)))
; #define LAS __attribute__((address_space(3)))
; #define LDS_WAIT() asm volatile("s_waitcnt lgkmcnt(0)" ::: "memory")
;     const int pr = item >> 1, kb = 2 * (pr / nblk) + (item & 1), nb = pr % nblk, k0 = 64 * kb, n0 = 32 * nb;
;     const int nr = n0 + (lane & 31); const int sc = MAP == 1 ? src_col_in(nr) : nr;
;     float v[32];
; #pragma unroll
;     for (int i = 0; i < 32; ++i) v[i] = sc >= 0 ? W[(size_t)(k0 + 2 * i + (lane >> 5)) * Nsrc + sc] : 0.f;
; #pragma unroll
;     for (int i = 0; i < 32; ++i) { const int k = k0 + 2 * i + (lane >> 5); float x = v[i] * wscale; if (KS) x *= (k < ksplit ? ksA[k] : ksB[k - ksplit]); scr[(2 * i + (lane >> 5)) * 33 + (lane & 31)] = x; }
;     LDS_WAIT(); asm volatile("" ::: "memory");
;     const int c = lane & 7;
; #pragma unroll
;     for (int j = 0; j < 4; ++j) { const int n = (lane >> 3) + 8 * j; const LAS float* s = scr + (8 * c) * 33 + n;
;         const unsigned long long o = (unsigned long long)pg8::pk4_fp8(s[0 * 33], s[1 * 33], s[2 * 33], s[3 * 33]) | ((unsigned long long)pg8::pk4_fp8(s[4 * 33], s[5 * 33], s[6 * 33], s[7 * 33]) << 32);
;         *(GAS unsigned long long*)(WT + (size_t)(n0 + n) * K + k0 + 8 * c) = o; }
;     LDS_WAIT(); asm volatile("" ::: "memory");
; }
; __global__ void __launch_bounds__(NWAVES * 64, 2) hybrid_fwd(Args args) {
;     ...
;             p0_transpose_item_f8<false>(args.in[16] + (size_t)l * FF * DM, FF, DM, DM / 32, (unsigned char*)(ws + WS_WDN + l * SZ_WDN), 128.f, args.in[16], args.in[16], 0, scr, r, lane);
	v_max_f32_e32 v226, v226, v226
	v_max_f32_e32 v227, v227, v227
	v_max_f32_e32 v228, v228, v228
	v_max_f32_e32 v229, v229, v229
	v_max_f32_e32 v230, v230, v230
	v_max_f32_e32 v231, v231, v231
	v_max_f32_e32 v232, v232, v232
	v_max_f32_e32 v233, v233, v233
	v_max_f32_e32 v234, v234, v234
	v_max_f32_e32 v235, v235, v235
	v_max_f32_e32 v236, v236, v236
	v_max_f32_e32 v237, v237, v237
	v_max_f32_e32 v238, v238, v238
	v_max_f32_e32 v239, v239, v239
	v_max_f32_e32 v240, v240, v240
	v_max_f32_e32 v241, v241, v241
	v_med3_f32 v226, v226, s62, v95
	v_med3_f32 v227, v227, s62, v95
	v_med3_f32 v228, v228, s62, v95
	v_med3_f32 v229, v229, s62, v95
	v_med3_f32 v230, v230, s62, v95
	v_med3_f32 v231, v231, s62, v95
	v_med3_f32 v232, v232, s62, v95
	v_med3_f32 v233, v233, s62, v95
	v_med3_f32 v234, v234, s62, v95
	v_med3_f32 v235, v235, s62, v95
	v_med3_f32 v236, v236, s62, v95
	v_med3_f32 v237, v237, s62, v95
	v_med3_f32 v238, v238, s62, v95
	v_med3_f32 v239, v239, s62, v95
	v_med3_f32 v240, v240, s62, v95
	v_med3_f32 v241, v241, s62, v95
	v_mov_b32_e32 v242, 0
	v_mov_b32_e32 v243, 0
	v_mov_b32_e32 v244, 0
	v_mov_b32_e32 v245, 0
	v_cvt_pk_fp8_f32 v242, v226, v227
	v_cvt_pk_fp8_f32 v243, v230, v231
	v_cvt_pk_fp8_f32 v244, v234, v235
	v_cvt_pk_fp8_f32 v245, v238, v239
	v_cvt_pk_fp8_f32 v242, v228, v229 op_sel:[0,0,1]
	v_cvt_pk_fp8_f32 v243, v232, v233 op_sel:[0,0,1]
	v_cvt_pk_fp8_f32 v244, v236, v237 op_sel:[0,0,1]
	v_cvt_pk_fp8_f32 v245, v240, v241 op_sel:[0,0,1]
	s_nop 0
	global_store_dwordx4 v80, v[242:245], s[6:7]
	s_waitcnt vmcnt(12)
	v_mul_f32_e32 v144, 0x43000000, v144
	v_mul_f32_e32 v145, 0x43000000, v145
	v_mul_f32_e32 v146, 0x43000000, v146
	v_mul_f32_e32 v147, 0x43000000, v147
	ds_write_b128 v209, v[144:147]
	v_mul_f32_e32 v148, 0x43000000, v148
	v_mul_f32_e32 v149, 0x43000000, v149
	v_mul_f32_e32 v150, 0x43000000, v150
	v_mul_f32_e32 v151, 0x43000000, v151
	ds_write_b128 v209, v[148:151] offset:1024
	v_mul_f32_e32 v152, 0x43000000, v152
	v_mul_f32_e32 v153, 0x43000000, v153
	v_mul_f32_e32 v154, 0x43000000, v154
	v_mul_f32_e32 v155, 0x43000000, v155
	ds_write_b128 v209, v[152:155] offset:2048
	v_mul_f32_e32 v156, 0x43000000, v156
	v_mul_f32_e32 v157, 0x43000000, v157
	v_mul_f32_e32 v158, 0x43000000, v158
	v_mul_f32_e32 v159, 0x43000000, v159
	ds_write_b128 v209, v[156:159] offset:3072
	v_mul_f32_e32 v160, 0x43000000, v160
	v_mul_f32_e32 v161, 0x43000000, v161
	v_mul_f32_e32 v162, 0x43000000, v162
	v_mul_f32_e32 v163, 0x43000000, v163
	ds_write_b128 v209, v[160:163] offset:4096
	v_mul_f32_e32 v164, 0x43000000, v164
	v_mul_f32_e32 v165, 0x43000000, v165
	v_mul_f32_e32 v166, 0x43000000, v166
	v_mul_f32_e32 v167, 0x43000000, v167
	ds_write_b128 v209, v[164:167] offset:5120
	v_mul_f32_e32 v168, 0x43000000, v168
	v_mul_f32_e32 v169, 0x43000000, v169
	v_mul_f32_e32 v170, 0x43000000, v170
	v_mul_f32_e32 v171, 0x43000000, v171
	ds_write_b128 v209, v[168:171] offset:6144
	v_mul_f32_e32 v172, 0x43000000, v172
	v_mul_f32_e32 v173, 0x43000000, v173
	v_mul_f32_e32 v174, 0x43000000, v174
	v_mul_f32_e32 v175, 0x43000000, v175
	ds_write_b128 v209, v[172:175] offset:7168
	s_waitcnt lgkmcnt(0)
	s_barrier
	s_add_u32 s8, s38, 0x8000000
	s_addc_u32 s9, s39, 0
	global_load_dwordx4 v[144:147], v75, s[8:9]
	s_add_u32 s8, s8, 0x8000
	s_addc_u32 s9, s9, 0
	global_load_dwordx4 v[148:151], v75, s[8:9]
	s_add_u32 s8, s8, 0x8000
	s_addc_u32 s9, s9, 0
	global_load_dwordx4 v[152:155], v75, s[8:9]
	s_add_u32 s8, s8, 0x8000
	s_addc_u32 s9, s9, 0
	global_load_dwordx4 v[156:159], v75, s[8:9]
	s_add_u32 s8, s8, 0x8000
	s_addc_u32 s9, s9, 0
	global_load_dwordx4 v[160:163], v75, s[8:9]
	s_add_u32 s8, s8, 0x8000
	s_addc_u32 s9, s9, 0
	global_load_dwordx4 v[164:167], v75, s[8:9]
	s_add_u32 s8, s8, 0x8000
	s_addc_u32 s9, s9, 0
	global_load_dwordx4 v[168:171], v75, s[8:9]
	s_add_u32 s8, s8, 0x8000
	s_addc_u32 s9, s9, 0
	global_load_dwordx4 v[172:175], v75, s[8:9]
	s_add_u32 s6, s40, 0x2001000
	s_addc_u32 s7, s41, 0
	ds_read_b32 v226, v211
	ds_read_b32 v227, v211 offset:512
	ds_read_b32 v228, v211 offset:1024
	ds_read_b32 v229, v211 offset:1536
	ds_read_b32 v230, v211 offset:2048
	ds_read_b32 v231, v211 offset:2560
	ds_read_b32 v232, v211 offset:3072
	ds_read_b32 v233, v211 offset:3584
	ds_read_b32 v234, v211 offset:4096
	ds_read_b32 v235, v211 offset:4608
	ds_read_b32 v236, v211 offset:5120
	ds_read_b32 v237, v211 offset:5632
	ds_read_b32 v238, v211 offset:6144
	ds_read_b32 v239, v211 offset:6656
	ds_read_b32 v240, v211 offset:7168
	ds_read_b32 v241, v211 offset:7680
	s_waitcnt lgkmcnt(0)
	v_max_f32_e32 v226, v226, v226
	v_max_f32_e32 v227, v227, v227
	v_max_f32_e32 v228, v228, v228
	v_max_f32_e32 v229, v229, v229
	v_max_f32_e32 v230, v230, v230
	v_max_f32_e32 v231, v231, v231
	v_max_f32_e32 v232, v232, v232
	v_max_f32_e32 v233, v233, v233
	v_max_f32_e32 v234, v234, v234
	v_max_f32_e32 v235, v235, v235
	v_max_f32_e32 v236, v236, v236
	v_max_f32_e32 v237, v237, v237
	v_max_f32_e32 v238, v238, v238
	v_max_f32_e32 v239, v239, v239
	v_max_f32_e32 v240, v240, v240
	v_max_f32_e32 v241, v241, v241
	v_med3_f32 v226, v226, s62, v95
	v_med3_f32 v227, v227, s62, v95
	v_med3_f32 v228, v228, s62, v95
	v_med3_f32 v229, v229, s62, v95
	v_med3_f32 v230, v230, s62, v95
	v_med3_f32 v231, v231, s62, v95
	v_med3_f32 v232, v232, s62, v95
	v_med3_f32 v233, v233, s62, v95
	v_med3_f32 v234, v234, s62, v95
	v_med3_f32 v235, v235, s62, v95
	v_med3_f32 v236, v236, s62, v95
	v_med3_f32 v237, v237, s62, v95
	v_med3_f32 v238, v238, s62, v95
	v_med3_f32 v239, v239, s62, v95
	v_med3_f32 v240, v240, s62, v95
	v_med3_f32 v241, v241, s62, v95
	v_mov_b32_e32 v242, 0
	v_mov_b32_e32 v243, 0
	v_mov_b32_e32 v244, 0
	v_mov_b32_e32 v245, 0
	v_cvt_pk_fp8_f32 v242, v226, v227
	v_cvt_pk_fp8_f32 v243, v230, v231
	v_cvt_pk_fp8_f32 v244, v234, v235
	v_cvt_pk_fp8_f32 v245, v238, v239
	v_cvt_pk_fp8_f32 v242, v228, v229 op_sel:[0,0,1]
	v_cvt_pk_fp8_f32 v243, v232, v233 op_sel:[0,0,1]
	v_cvt_pk_fp8_f32 v244, v236, v237 op_sel:[0,0,1]
	v_cvt_pk_fp8_f32 v245, v240, v241 op_sel:[0,0,1]
	s_nop 0
	global_store_dwordx4 v79, v[242:245], s[6:7]
	ds_read_b32 v226, v213
	ds_read_b32 v227, v213 offset:512
	ds_read_b32 v228, v213 offset:1024
	ds_read_b32 v229, v213 offset:1536
	ds_read_b32 v230, v213 offset:2048
	ds_read_b32 v231, v213 offset:2560
	ds_read_b32 v232, v213 offset:3072
	ds_read_b32 v233, v213 offset:3584
	ds_read_b32 v234, v213 offset:4096
	ds_read_b32 v235, v213 offset:4608
	ds_read_b32 v236, v213 offset:5120
	ds_read_b32 v237, v213 offset:5632
	ds_read_b32 v238, v213 offset:6144
	ds_read_b32 v239, v213 offset:6656
	ds_read_b32 v240, v213 offset:7168
	ds_read_b32 v241, v213 offset:7680
	s_waitcnt lgkmcnt(0)
; #define GAS __attribute__((address_space(1)))
; #define LAS __attribute__((address_space(3)))
; #define LDS_WAIT() asm volatile("s_waitcnt lgkmcnt(0)" ::: "memory")
;     const int pr = item >> 1, kb = 2 * (pr / nblk) + (item & 1), nb = pr % nblk, k0 = 64 * kb, n0 = 32 * nb;
;     const int nr = n0 + (lane & 31); const int sc = MAP == 1 ? src_col_in(nr) : nr;
;     float v[32];
; #pragma unroll
;     for (int i = 0; i < 32; ++i) v[i] = sc >= 0 ? W[(size_t)(k0 + 2 * i + (lane >> 5)) * Nsrc + sc] : 0.f;
; #pragma unroll
;     for (int i = 0; i < 32; ++i) { const int k = k0 + 2 * i + (lane >> 5); float x = v[i] * wscale; if (KS) x *= (k < ksplit ? ksA[k] : ksB[k - ksplit]); scr[(2 * i + (lane >> 5)) * 33 + (lane & 31)] = x; }
;     LDS_WAIT(); asm volatile("" ::: "memory");
;     const int c = lane & 7;
; #pragma unroll
;     for (int j = 0; j < 4; ++j) { const int n = (lane >> 3) + 8 * j; const LAS float* s = scr + (8 * c) * 33 + n;
;         const unsigned long long o = (unsigned long long)pg8::pk4_fp8(s[0 * 33], s[1 * 33], s[2 * 33], s[3 * 33]) | ((unsigned long long)pg8::pk4_fp8(s[4 * 33], s[5 * 33], s[6 * 33], s[7 * 33]) << 32);
;         *(GAS unsigned long long*)(WT + (size_t)(n0 + n) * K + k0 + 8 * c) = o; }
;     LDS_WAIT(); asm volatile("" ::: "memory");
; }
; __global__ void __launch_bounds__(NWAVES * 64, 2) hybrid_fwd(Args args) {
;     ...
;             p0_transpose_item_f8<false>(args.in[16] + (size_t)l * FF * DM, FF, DM, DM / 32, (unsigned char*)(ws + WS_WDN + l * SZ_WDN), 128.f, args.in[16], args.in[16], 0, scr, r, lane);
	v_max_f32_e32 v226, v226, v226
	v_max_f32_e32 v227, v227, v227
	v_max_f32_e32 v228, v228, v228
	v_max_f32_e32 v229, v229, v229
	v_max_f32_e32 v230, v230, v230
	v_max_f32_e32 v231, v231, v231
	v_max_f32_e32 v232, v232, v232
	v_max_f32_e32 v233, v233, v233
	v_max_f32_e32 v234, v234, v234
	v_max_f32_e32 v235, v235, v235
	v_max_f32_e32 v236, v236, v236
	v_max_f32_e32 v237, v237, v237
	v_max_f32_e32 v238, v238, v238
	v_max_f32_e32 v239, v239, v239
	v_max_f32_e32 v240, v240, v240
	v_max_f32_e32 v241, v241, v241
	v_med3_f32 v226, v226, s62, v95
	v_med3_f32 v227, v227, s62, v95
	v_med3_f32 v228, v228, s62, v95
	v_med3_f32 v229, v229, s62, v95
	v_med3_f32 v230, v230, s62, v95
	v_med3_f32 v231, v231, s62, v95
	v_med3_f32 v232, v232, s62, v95
	v_med3_f32 v233, v233, s62, v95
	v_med3_f32 v234, v234, s62, v95
	v_med3_f32 v235, v235, s62, v95
	v_med3_f32 v236, v236, s62, v95
	v_med3_f32 v237, v237, s62, v95
	v_med3_f32 v238, v238, s62, v95
	v_med3_f32 v239, v239, s62, v95
	v_med3_f32 v240, v240, s62, v95
	v_med3_f32 v241, v241, s62, v95
	v_mov_b32_e32 v242, 0
	v_mov_b32_e32 v243, 0
	v_mov_b32_e32 v244, 0
	v_mov_b32_e32 v245, 0
	v_cvt_pk_fp8_f32 v242, v226, v227
	v_cvt_pk_fp8_f32 v243, v230, v231
	v_cvt_pk_fp8_f32 v244, v234, v235
	v_cvt_pk_fp8_f32 v245, v238, v239
	v_cvt_pk_fp8_f32 v242, v228, v229 op_sel:[0,0,1]
	v_cvt_pk_fp8_f32 v243, v232, v233 op_sel:[0,0,1]
	v_cvt_pk_fp8_f32 v244, v236, v237 op_sel:[0,0,1]
	v_cvt_pk_fp8_f32 v245, v240, v241 op_sel:[0,0,1]
	s_nop 0
	global_store_dwordx4 v80, v[242:245], s[6:7]
	s_waitcnt vmcnt(12)
	v_mul_f32_e32 v176, 0x43000000, v176
	v_mul_f32_e32 v177, 0x43000000, v177
	v_mul_f32_e32 v178, 0x43000000, v178
	v_mul_f32_e32 v179, 0x43000000, v179
	ds_write_b128 v210, v[176:179]
	v_mul_f32_e32 v180, 0x43000000, v180
	v_mul_f32_e32 v181, 0x43000000, v181
	v_mul_f32_e32 v182, 0x43000000, v182
	v_mul_f32_e32 v183, 0x43000000, v183
	ds_write_b128 v210, v[180:183] offset:1024
	v_mul_f32_e32 v184, 0x43000000, v184
	v_mul_f32_e32 v185, 0x43000000, v185
	v_mul_f32_e32 v186, 0x43000000, v186
	v_mul_f32_e32 v187, 0x43000000, v187
	ds_write_b128 v210, v[184:187] offset:2048
	v_mul_f32_e32 v188, 0x43000000, v188
	v_mul_f32_e32 v189, 0x43000000, v189
	v_mul_f32_e32 v190, 0x43000000, v190
	v_mul_f32_e32 v191, 0x43000000, v191
	ds_write_b128 v210, v[188:191] offset:3072
	v_mul_f32_e32 v192, 0x43000000, v192
	v_mul_f32_e32 v193, 0x43000000, v193
	v_mul_f32_e32 v194, 0x43000000, v194
	v_mul_f32_e32 v195, 0x43000000, v195
	ds_write_b128 v210, v[192:195] offset:4096
	v_mul_f32_e32 v196, 0x43000000, v196
	v_mul_f32_e32 v197, 0x43000000, v197
	v_mul_f32_e32 v198, 0x43000000, v198
	v_mul_f32_e32 v199, 0x43000000, v199
	ds_write_b128 v210, v[196:199] offset:5120
	v_mul_f32_e32 v200, 0x43000000, v200
	v_mul_f32_e32 v201, 0x43000000, v201
	v_mul_f32_e32 v202, 0x43000000, v202
	v_mul_f32_e32 v203, 0x43000000, v203
	ds_write_b128 v210, v[200:203] offset:6144
	v_mul_f32_e32 v204, 0x43000000, v204
	v_mul_f32_e32 v205, 0x43000000, v205
	v_mul_f32_e32 v206, 0x43000000, v206
	v_mul_f32_e32 v207, 0x43000000, v207
	ds_write_b128 v210, v[204:207] offset:7168
	s_waitcnt lgkmcnt(0)
	s_barrier
	s_add_u32 s8, s38, 0x8001000
	s_addc_u32 s9, s39, 0
	global_load_dwordx4 v[176:179], v75, s[8:9]
	s_add_u32 s8, s8, 0x8000
	s_addc_u32 s9, s9, 0
	global_load_dwordx4 v[180:183], v75, s[8:9]
	s_add_u32 s8, s8, 0x8000
	s_addc_u32 s9, s9, 0
	global_load_dwordx4 v[184:187], v75, s[8:9]
	s_add_u32 s8, s8, 0x8000
	s_addc_u32 s9, s9, 0
	global_load_dwordx4 v[188:191], v75, s[8:9]
	s_add_u32 s8, s8, 0x8000
	s_addc_u32 s9, s9, 0
	global_load_dwordx4 v[192:195], v75, s[8:9]
	s_add_u32 s8, s8, 0x8000
	s_addc_u32 s9, s9, 0
	global_load_dwordx4 v[196:199], v75, s[8:9]
	s_add_u32 s8, s8, 0x8000
	s_addc_u32 s9, s9, 0
	global_load_dwordx4 v[200:203], v75, s[8:9]
	s_add_u32 s8, s8, 0x8000
	s_addc_u32 s9, s9, 0
	global_load_dwordx4 v[204:207], v75, s[8:9]
	s_add_u32 s6, s40, 0x3001000
	s_addc_u32 s7, s41, 0
	ds_read_b32 v226, v212
	ds_read_b32 v227, v212 offset:512
	ds_read_b32 v228, v212 offset:1024
	ds_read_b32 v229, v212 offset:1536
	ds_read_b32 v230, v212 offset:2048
	ds_read_b32 v231, v212 offset:2560
	ds_read_b32 v232, v212 offset:3072
	ds_read_b32 v233, v212 offset:3584
	ds_read_b32 v234, v212 offset:4096
	ds_read_b32 v235, v212 offset:4608
	ds_read_b32 v236, v212 offset:5120
	ds_read_b32 v237, v212 offset:5632
	ds_read_b32 v238, v212 offset:6144
	ds_read_b32 v239, v212 offset:6656
	ds_read_b32 v240, v212 offset:7168
	ds_read_b32 v241, v212 offset:7680
	s_waitcnt lgkmcnt(0)
	v_max_f32_e32 v226, v226, v226
	v_max_f32_e32 v227, v227, v227
	v_max_f32_e32 v228, v228, v228
	v_max_f32_e32 v229, v229, v229
	v_max_f32_e32 v230, v230, v230
	v_max_f32_e32 v231, v231, v231
	v_max_f32_e32 v232, v232, v232
	v_max_f32_e32 v233, v233, v233
	v_max_f32_e32 v234, v234, v234
	v_max_f32_e32 v235, v235, v235
	v_max_f32_e32 v236, v236, v236
	v_max_f32_e32 v237, v237, v237
	v_max_f32_e32 v238, v238, v238
	v_max_f32_e32 v239, v239, v239
	v_max_f32_e32 v240, v240, v240
	v_max_f32_e32 v241, v241, v241
	v_med3_f32 v226, v226, s62, v95
	v_med3_f32 v227, v227, s62, v95
	v_med3_f32 v228, v228, s62, v95
	v_med3_f32 v229, v229, s62, v95
	v_med3_f32 v230, v230, s62, v95
	v_med3_f32 v231, v231, s62, v95
	v_med3_f32 v232, v232, s62, v95
	v_med3_f32 v233, v233, s62, v95
	v_med3_f32 v234, v234, s62, v95
	v_med3_f32 v235, v235, s62, v95
	v_med3_f32 v236, v236, s62, v95
	v_med3_f32 v237, v237, s62, v95
	v_med3_f32 v238, v238, s62, v95
	v_med3_f32 v239, v239, s62, v95
	v_med3_f32 v240, v240, s62, v95
	v_med3_f32 v241, v241, s62, v95
	v_mov_b32_e32 v242, 0
	v_mov_b32_e32 v243, 0
	v_mov_b32_e32 v244, 0
	v_mov_b32_e32 v245, 0
	v_cvt_pk_fp8_f32 v242, v226, v227
	v_cvt_pk_fp8_f32 v243, v230, v231
	v_cvt_pk_fp8_f32 v244, v234, v235
	v_cvt_pk_fp8_f32 v245, v238, v239
	v_cvt_pk_fp8_f32 v242, v228, v229 op_sel:[0,0,1]
	v_cvt_pk_fp8_f32 v243, v232, v233 op_sel:[0,0,1]
	v_cvt_pk_fp8_f32 v244, v236, v237 op_sel:[0,0,1]
	v_cvt_pk_fp8_f32 v245, v240, v241 op_sel:[0,0,1]
	s_nop 0
	global_store_dwordx4 v79, v[242:245], s[6:7]
	ds_read_b32 v226, v214
	ds_read_b32 v227, v214 offset:512
	ds_read_b32 v228, v214 offset:1024
	ds_read_b32 v229, v214 offset:1536
	ds_read_b32 v230, v214 offset:2048
	ds_read_b32 v231, v214 offset:2560
	ds_read_b32 v232, v214 offset:3072
	ds_read_b32 v233, v214 offset:3584
	ds_read_b32 v234, v214 offset:4096
	ds_read_b32 v235, v214 offset:4608
	ds_read_b32 v236, v214 offset:5120
	ds_read_b32 v237, v214 offset:5632
	ds_read_b32 v238, v214 offset:6144
	ds_read_b32 v239, v214 offset:6656
	ds_read_b32 v240, v214 offset:7168
	ds_read_b32 v241, v214 offset:7680
	s_waitcnt lgkmcnt(0)
; #define GAS __attribute__((address_space(1)))
; #define LAS __attribute__((address_space(3)))
; #define LDS_WAIT() asm volatile("s_waitcnt lgkmcnt(0)" ::: "memory")
;     const int pr = item >> 1, kb = 2 * (pr / nblk) + (item & 1), nb = pr % nblk, k0 = 64 * kb, n0 = 32 * nb;
;     const int nr = n0 + (lane & 31); const int sc = MAP == 1 ? src_col_in(nr) : nr;
;     float v[32];
; #pragma unroll
;     for (int i = 0; i < 32; ++i) v[i] = sc >= 0 ? W[(size_t)(k0 + 2 * i + (lane >> 5)) * Nsrc + sc] : 0.f;
; #pragma unroll
;     for (int i = 0; i < 32; ++i) { const int k = k0 + 2 * i + (lane >> 5); float x = v[i] * wscale; if (KS) x *= (k < ksplit ? ksA[k] : ksB[k - ksplit]); scr[(2 * i + (lane >> 5)) * 33 + (lane & 31)] = x; }
;     LDS_WAIT(); asm volatile("" ::: "memory");
;     const int c = lane & 7;
; #pragma unroll
;     for (int j = 0; j < 4; ++j) { const int n = (lane >> 3) + 8 * j; const LAS float* s = scr + (8 * c) * 33 + n;
;         const unsigned long long o = (unsigned long long)pg8::pk4_fp8(s[0 * 33], s[1 * 33], s[2 * 33], s[3 * 33]) | ((unsigned long long)pg8::pk4_fp8(s[4 * 33], s[5 * 33], s[6 * 33], s[7 * 33]) << 32);
;         *(GAS unsigned long long*)(WT + (size_t)(n0 + n) * K + k0 + 8 * c) = o; }
;     LDS_WAIT(); asm volatile("" ::: "memory");
; }
; __global__ void __launch_bounds__(NWAVES * 64, 2) hybrid_fwd(Args args) {
;     ...
;             p0_transpose_item_f8<false>(args.in[16] + (size_t)l * FF * DM, FF, DM, DM / 32, (unsigned char*)(ws + WS_WDN + l * SZ_WDN), 128.f, args.in[16], args.in[16], 0, scr, r, lane);
	v_max_f32_e32 v226, v226, v226
	v_max_f32_e32 v227, v227, v227
	v_max_f32_e32 v228, v228, v228
	v_max_f32_e32 v229, v229, v229
	v_max_f32_e32 v230, v230, v230
	v_max_f32_e32 v231, v231, v231
	v_max_f32_e32 v232, v232, v232
	v_max_f32_e32 v233, v233, v233
	v_max_f32_e32 v234, v234, v234
	v_max_f32_e32 v235, v235, v235
	v_max_f32_e32 v236, v236, v236
	v_max_f32_e32 v237, v237, v237
	v_max_f32_e32 v238, v238, v238
	v_max_f32_e32 v239, v239, v239
	v_max_f32_e32 v240, v240, v240
	v_max_f32_e32 v241, v241, v241
	v_med3_f32 v226, v226, s62, v95
	v_med3_f32 v227, v227, s62, v95
	v_med3_f32 v228, v228, s62, v95
	v_med3_f32 v229, v229, s62, v95
	v_med3_f32 v230, v230, s62, v95
	v_med3_f32 v231, v231, s62, v95
	v_med3_f32 v232, v232, s62, v95
	v_med3_f32 v233, v233, s62, v95
	v_med3_f32 v234, v234, s62, v95
	v_med3_f32 v235, v235, s62, v95
	v_med3_f32 v236, v236, s62, v95
	v_med3_f32 v237, v237, s62, v95
	v_med3_f32 v238, v238, s62, v95
	v_med3_f32 v239, v239, s62, v95
	v_med3_f32 v240, v240, s62, v95
	v_med3_f32 v241, v241, s62, v95
	v_mov_b32_e32 v242, 0
	v_mov_b32_e32 v243, 0
	v_mov_b32_e32 v244, 0
	v_mov_b32_e32 v245, 0
	v_cvt_pk_fp8_f32 v242, v226, v227
	v_cvt_pk_fp8_f32 v243, v230, v231
	v_cvt_pk_fp8_f32 v244, v234, v235
	v_cvt_pk_fp8_f32 v245, v238, v239
	v_cvt_pk_fp8_f32 v242, v228, v229 op_sel:[0,0,1]
	v_cvt_pk_fp8_f32 v243, v232, v233 op_sel:[0,0,1]
	v_cvt_pk_fp8_f32 v244, v236, v237 op_sel:[0,0,1]
	v_cvt_pk_fp8_f32 v245, v240, v241 op_sel:[0,0,1]
	s_nop 0
	global_store_dwordx4 v80, v[242:245], s[6:7]
	s_waitcnt vmcnt(12)
	v_mul_f32_e32 v144, 0x43000000, v144
	v_mul_f32_e32 v145, 0x43000000, v145
	v_mul_f32_e32 v146, 0x43000000, v146
	v_mul_f32_e32 v147, 0x43000000, v147
	ds_write_b128 v209, v[144:147]
	v_mul_f32_e32 v148, 0x43000000, v148
	v_mul_f32_e32 v149, 0x43000000, v149
	v_mul_f32_e32 v150, 0x43000000, v150
	v_mul_f32_e32 v151, 0x43000000, v151
	ds_write_b128 v209, v[148:151] offset:1024
	v_mul_f32_e32 v152, 0x43000000, v152
	v_mul_f32_e32 v153, 0x43000000, v153
	v_mul_f32_e32 v154, 0x43000000, v154
	v_mul_f32_e32 v155, 0x43000000, v155
	ds_write_b128 v209, v[152:155] offset:2048
	v_mul_f32_e32 v156, 0x43000000, v156
	v_mul_f32_e32 v157, 0x43000000, v157
	v_mul_f32_e32 v158, 0x43000000, v158
	v_mul_f32_e32 v159, 0x43000000, v159
	ds_write_b128 v209, v[156:159] offset:3072
	v_mul_f32_e32 v160, 0x43000000, v160
	v_mul_f32_e32 v161, 0x43000000, v161
	v_mul_f32_e32 v162, 0x43000000, v162
	v_mul_f32_e32 v163, 0x43000000, v163
	ds_write_b128 v209, v[160:163] offset:4096
	v_mul_f32_e32 v164, 0x43000000, v164
	v_mul_f32_e32 v165, 0x43000000, v165
	v_mul_f32_e32 v166, 0x43000000, v166
	v_mul_f32_e32 v167, 0x43000000, v167
	ds_write_b128 v209, v[164:167] offset:5120
	v_mul_f32_e32 v168, 0x43000000, v168
	v_mul_f32_e32 v169, 0x43000000, v169
	v_mul_f32_e32 v170, 0x43000000, v170
	v_mul_f32_e32 v171, 0x43000000, v171
	ds_write_b128 v209, v[168:171] offset:6144
	v_mul_f32_e32 v172, 0x43000000, v172
	v_mul_f32_e32 v173, 0x43000000, v173
	v_mul_f32_e32 v174, 0x43000000, v174
	v_mul_f32_e32 v175, 0x43000000, v175
	ds_write_b128 v209, v[172:175] offset:7168
	s_waitcnt lgkmcnt(0)
	s_barrier
	s_add_u32 s8, s38, 0x8002000
	s_addc_u32 s9, s39, 0
	global_load_dwordx4 v[144:147], v75, s[8:9]
	s_add_u32 s8, s8, 0x8000
	s_addc_u32 s9, s9, 0
	global_load_dwordx4 v[148:151], v75, s[8:9]
	s_add_u32 s8, s8, 0x8000
	s_addc_u32 s9, s9, 0
	global_load_dwordx4 v[152:155], v75, s[8:9]
	s_add_u32 s8, s8, 0x8000
	s_addc_u32 s9, s9, 0
	global_load_dwordx4 v[156:159], v75, s[8:9]
	s_add_u32 s8, s8, 0x8000
	s_addc_u32 s9, s9, 0
	global_load_dwordx4 v[160:163], v75, s[8:9]
	s_add_u32 s8, s8, 0x8000
	s_addc_u32 s9, s9, 0
	global_load_dwordx4 v[164:167], v75, s[8:9]
	s_add_u32 s8, s8, 0x8000
	s_addc_u32 s9, s9, 0
	global_load_dwordx4 v[168:171], v75, s[8:9]
	s_add_u32 s8, s8, 0x8000
	s_addc_u32 s9, s9, 0
	global_load_dwordx4 v[172:175], v75, s[8:9]
	s_add_u32 s6, s40, 0x2000
	s_addc_u32 s7, s41, 0
	ds_read_b32 v226, v211
	ds_read_b32 v227, v211 offset:512
	ds_read_b32 v228, v211 offset:1024
	ds_read_b32 v229, v211 offset:1536
	ds_read_b32 v230, v211 offset:2048
	ds_read_b32 v231, v211 offset:2560
	ds_read_b32 v232, v211 offset:3072
	ds_read_b32 v233, v211 offset:3584
	ds_read_b32 v234, v211 offset:4096
	ds_read_b32 v235, v211 offset:4608
	ds_read_b32 v236, v211 offset:5120
	ds_read_b32 v237, v211 offset:5632
	ds_read_b32 v238, v211 offset:6144
	ds_read_b32 v239, v211 offset:6656
	ds_read_b32 v240, v211 offset:7168
	ds_read_b32 v241, v211 offset:7680
	s_waitcnt lgkmcnt(0)
	v_max_f32_e32 v226, v226, v226
	v_max_f32_e32 v227, v227, v227
	v_max_f32_e32 v228, v228, v228
	v_max_f32_e32 v229, v229, v229
	v_max_f32_e32 v230, v230, v230
	v_max_f32_e32 v231, v231, v231
	v_max_f32_e32 v232, v232, v232
	v_max_f32_e32 v233, v233, v233
	v_max_f32_e32 v234, v234, v234
	v_max_f32_e32 v235, v235, v235
	v_max_f32_e32 v236, v236, v236
	v_max_f32_e32 v237, v237, v237
	v_max_f32_e32 v238, v238, v238
	v_max_f32_e32 v239, v239, v239
	v_max_f32_e32 v240, v240, v240
	v_max_f32_e32 v241, v241, v241
	v_med3_f32 v226, v226, s62, v95
	v_med3_f32 v227, v227, s62, v95
	v_med3_f32 v228, v228, s62, v95
	v_med3_f32 v229, v229, s62, v95
	v_med3_f32 v230, v230, s62, v95
	v_med3_f32 v231, v231, s62, v95
	v_med3_f32 v232, v232, s62, v95
	v_med3_f32 v233, v233, s62, v95
	v_med3_f32 v234, v234, s62, v95
	v_med3_f32 v235, v235, s62, v95
	v_med3_f32 v236, v236, s62, v95
	v_med3_f32 v237, v237, s62, v95
	v_med3_f32 v238, v238, s62, v95
	v_med3_f32 v239, v239, s62, v95
	v_med3_f32 v240, v240, s62, v95
	v_med3_f32 v241, v241, s62, v95
	v_mov_b32_e32 v242, 0
	v_mov_b32_e32 v243, 0
	v_mov_b32_e32 v244, 0
	v_mov_b32_e32 v245, 0
	v_cvt_pk_fp8_f32 v242, v226, v227
	v_cvt_pk_fp8_f32 v243, v230, v231
	v_cvt_pk_fp8_f32 v244, v234, v235
	v_cvt_pk_fp8_f32 v245, v238, v239
	v_cvt_pk_fp8_f32 v242, v228, v229 op_sel:[0,0,1]
	v_cvt_pk_fp8_f32 v243, v232, v233 op_sel:[0,0,1]
	v_cvt_pk_fp8_f32 v244, v236, v237 op_sel:[0,0,1]
	v_cvt_pk_fp8_f32 v245, v240, v241 op_sel:[0,0,1]
	s_nop 0
	global_store_dwordx4 v79, v[242:245], s[6:7]
	ds_read_b32 v226, v213
	ds_read_b32 v227, v213 offset:512
	ds_read_b32 v228, v213 offset:1024
	ds_read_b32 v229, v213 offset:1536
	ds_read_b32 v230, v213 offset:2048
	ds_read_b32 v231, v213 offset:2560
	ds_read_b32 v232, v213 offset:3072
	ds_read_b32 v233, v213 offset:3584
	ds_read_b32 v234, v213 offset:4096
	ds_read_b32 v235, v213 offset:4608
	ds_read_b32 v236, v213 offset:5120
	ds_read_b32 v237, v213 offset:5632
	ds_read_b32 v238, v213 offset:6144
	ds_read_b32 v239, v213 offset:6656
	ds_read_b32 v240, v213 offset:7168
	ds_read_b32 v241, v213 offset:7680
	s_waitcnt lgkmcnt(0)
; #define GAS __attribute__((address_space(1)))
; #define LAS __attribute__((address_space(3)))
; #define LDS_WAIT() asm volatile("s_waitcnt lgkmcnt(0)" ::: "memory")
;     const int pr = item >> 1, kb = 2 * (pr / nblk) + (item & 1), nb = pr % nblk, k0 = 64 * kb, n0 = 32 * nb;
;     const int nr = n0 + (lane & 31); const int sc = MAP == 1 ? src_col_in(nr) : nr;
;     float v[32];
; #pragma unroll
;     for (int i = 0; i < 32; ++i) v[i] = sc >= 0 ? W[(size_t)(k0 + 2 * i + (lane >> 5)) * Nsrc + sc] : 0.f;
; #pragma unroll
;     for (int i = 0; i < 32; ++i) { const int k = k0 + 2 * i + (lane >> 5); float x = v[i] * wscale; if (KS) x *= (k < ksplit ? ksA[k] : ksB[k - ksplit]); scr[(2 * i + (lane >> 5)) * 33 + (lane & 31)] = x; }
;     LDS_WAIT(); asm volatile("" ::: "memory");
;     const int c = lane & 7;
; #pragma unroll
;     for (int j = 0; j < 4; ++j) { const int n = (lane >> 3) + 8 * j; const LAS float* s = scr + (8 * c) * 33 + n;
;         const unsigned long long o = (unsigned long long)pg8::pk4_fp8(s[0 * 33], s[1 * 33], s[2 * 33], s[3 * 33]) | ((unsigned long long)pg8::pk4_fp8(s[4 * 33], s[5 * 33], s[6 * 33], s[7 * 33]) << 32);
;         *(GAS unsigned long long*)(WT + (size_t)(n0 + n) * K + k0 + 8 * c) = o; }
;     LDS_WAIT(); asm volatile("" ::: "memory");
; }
; __global__ void __launch_bounds__(NWAVES * 64, 2) hybrid_fwd(Args args) {
;     ...
;             p0_transpose_item_f8<false>(args.in[16] + (size_t)l * FF * DM, FF, DM, DM / 32, (unsigned char*)(ws + WS_WDN + l * SZ_WDN), 128.f, args.in[16], args.in[16], 0, scr, r, lane);
	v_max_f32_e32 v226, v226, v226
	v_max_f32_e32 v227, v227, v227
	v_max_f32_e32 v228, v228, v228
	v_max_f32_e32 v229, v229, v229
	v_max_f32_e32 v230, v230, v230
	v_max_f32_e32 v231, v231, v231
	v_max_f32_e32 v232, v232, v232
	v_max_f32_e32 v233, v233, v233
	v_max_f32_e32 v234, v234, v234
	v_max_f32_e32 v235, v235, v235
	v_max_f32_e32 v236, v236, v236
	v_max_f32_e32 v237, v237, v237
	v_max_f32_e32 v238, v238, v238
	v_max_f32_e32 v239, v239, v239
	v_max_f32_e32 v240, v240, v240
	v_max_f32_e32 v241, v241, v241
	v_med3_f32 v226, v226, s62, v95
	v_med3_f32 v227, v227, s62, v95
	v_med3_f32 v228, v228, s62, v95
	v_med3_f32 v229, v229, s62, v95
	v_med3_f32 v230, v230, s62, v95
	v_med3_f32 v231, v231, s62, v95
	v_med3_f32 v232, v232, s62, v95
	v_med3_f32 v233, v233, s62, v95
	v_med3_f32 v234, v234, s62, v95
	v_med3_f32 v235, v235, s62, v95
	v_med3_f32 v236, v236, s62, v95
	v_med3_f32 v237, v237, s62, v95
	v_med3_f32 v238, v238, s62, v95
	v_med3_f32 v239, v239, s62, v95
	v_med3_f32 v240, v240, s62, v95
	v_med3_f32 v241, v241, s62, v95
	v_mov_b32_e32 v242, 0
	v_mov_b32_e32 v243, 0
	v_mov_b32_e32 v244, 0
	v_mov_b32_e32 v245, 0
	v_cvt_pk_fp8_f32 v242, v226, v227
	v_cvt_pk_fp8_f32 v243, v230, v231
	v_cvt_pk_fp8_f32 v244, v234, v235
	v_cvt_pk_fp8_f32 v245, v238, v239
	v_cvt_pk_fp8_f32 v242, v228, v229 op_sel:[0,0,1]
	v_cvt_pk_fp8_f32 v243, v232, v233 op_sel:[0,0,1]
	v_cvt_pk_fp8_f32 v244, v236, v237 op_sel:[0,0,1]
	v_cvt_pk_fp8_f32 v245, v240, v241 op_sel:[0,0,1]
	s_nop 0
	global_store_dwordx4 v80, v[242:245], s[6:7]
	s_waitcnt vmcnt(12)
	v_mul_f32_e32 v176, 0x43000000, v176
	v_mul_f32_e32 v177, 0x43000000, v177
	v_mul_f32_e32 v178, 0x43000000, v178
	v_mul_f32_e32 v179, 0x43000000, v179
	ds_write_b128 v210, v[176:179]
	v_mul_f32_e32 v180, 0x43000000, v180
	v_mul_f32_e32 v181, 0x43000000, v181
	v_mul_f32_e32 v182, 0x43000000, v182
	v_mul_f32_e32 v183, 0x43000000, v183
	ds_write_b128 v210, v[180:183] offset:1024
	v_mul_f32_e32 v184, 0x43000000, v184
	v_mul_f32_e32 v185, 0x43000000, v185
	v_mul_f32_e32 v186, 0x43000000, v186
	v_mul_f32_e32 v187, 0x43000000, v187
	ds_write_b128 v210, v[184:187] offset:2048
	v_mul_f32_e32 v188, 0x43000000, v188
	v_mul_f32_e32 v189, 0x43000000, v189
	v_mul_f32_e32 v190, 0x43000000, v190
	v_mul_f32_e32 v191, 0x43000000, v191
	ds_write_b128 v210, v[188:191] offset:3072
	v_mul_f32_e32 v192, 0x43000000, v192
	v_mul_f32_e32 v193, 0x43000000, v193
	v_mul_f32_e32 v194, 0x43000000, v194
	v_mul_f32_e32 v195, 0x43000000, v195
	ds_write_b128 v210, v[192:195] offset:4096
	v_mul_f32_e32 v196, 0x43000000, v196
	v_mul_f32_e32 v197, 0x43000000, v197
	v_mul_f32_e32 v198, 0x43000000, v198
	v_mul_f32_e32 v199, 0x43000000, v199
	ds_write_b128 v210, v[196:199] offset:5120
	v_mul_f32_e32 v200, 0x43000000, v200
	v_mul_f32_e32 v201, 0x43000000, v201
	v_mul_f32_e32 v202, 0x43000000, v202
	v_mul_f32_e32 v203, 0x43000000, v203
	ds_write_b128 v210, v[200:203] offset:6144
	v_mul_f32_e32 v204, 0x43000000, v204
	v_mul_f32_e32 v205, 0x43000000, v205
	v_mul_f32_e32 v206, 0x43000000, v206
	v_mul_f32_e32 v207, 0x43000000, v207
	ds_write_b128 v210, v[204:207] offset:7168
	s_waitcnt lgkmcnt(0)
	s_barrier
	s_add_u32 s8, s38, 0x8003000
	s_addc_u32 s9, s39, 0
	global_load_dwordx4 v[176:179], v75, s[8:9]
	s_add_u32 s8, s8, 0x8000
	s_addc_u32 s9, s9, 0
	global_load_dwordx4 v[180:183], v75, s[8:9]
	s_add_u32 s8, s8, 0x8000
	s_addc_u32 s9, s9, 0
	global_load_dwordx4 v[184:187], v75, s[8:9]
	s_add_u32 s8, s8, 0x8000
	s_addc_u32 s9, s9, 0
	global_load_dwordx4 v[188:191], v75, s[8:9]
	s_add_u32 s8, s8, 0x8000
	s_addc_u32 s9, s9, 0
	global_load_dwordx4 v[192:195], v75, s[8:9]
	s_add_u32 s8, s8, 0x8000
	s_addc_u32 s9, s9, 0
	global_load_dwordx4 v[196:199], v75, s[8:9]
	s_add_u32 s8, s8, 0x8000
	s_addc_u32 s9, s9, 0
	global_load_dwordx4 v[200:203], v75, s[8:9]
	s_add_u32 s8, s8, 0x8000
	s_addc_u32 s9, s9, 0
	global_load_dwordx4 v[204:207], v75, s[8:9]
	s_add_u32 s6, s40, 0x1002000
	s_addc_u32 s7, s41, 0
	ds_read_b32 v226, v212
	ds_read_b32 v227, v212 offset:512
	ds_read_b32 v228, v212 offset:1024
	ds_read_b32 v229, v212 offset:1536
	ds_read_b32 v230, v212 offset:2048
	ds_read_b32 v231, v212 offset:2560
	ds_read_b32 v232, v212 offset:3072
	ds_read_b32 v233, v212 offset:3584
	ds_read_b32 v234, v212 offset:4096
	ds_read_b32 v235, v212 offset:4608
	ds_read_b32 v236, v212 offset:5120
	ds_read_b32 v237, v212 offset:5632
	ds_read_b32 v238, v212 offset:6144
	ds_read_b32 v239, v212 offset:6656
	ds_read_b32 v240, v212 offset:7168
	ds_read_b32 v241, v212 offset:7680
	s_waitcnt lgkmcnt(0)
	v_max_f32_e32 v226, v226, v226
	v_max_f32_e32 v227, v227, v227
	v_max_f32_e32 v228, v228, v228
	v_max_f32_e32 v229, v229, v229
	v_max_f32_e32 v230, v230, v230
	v_max_f32_e32 v231, v231, v231
	v_max_f32_e32 v232, v232, v232
	v_max_f32_e32 v233, v233, v233
	v_max_f32_e32 v234, v234, v234
	v_max_f32_e32 v235, v235, v235
	v_max_f32_e32 v236, v236, v236
	v_max_f32_e32 v237, v237, v237
	v_max_f32_e32 v238, v238, v238
	v_max_f32_e32 v239, v239, v239
	v_max_f32_e32 v240, v240, v240
	v_max_f32_e32 v241, v241, v241
	v_med3_f32 v226, v226, s62, v95
	v_med3_f32 v227, v227, s62, v95
	v_med3_f32 v228, v228, s62, v95
	v_med3_f32 v229, v229, s62, v95
	v_med3_f32 v230, v230, s62, v95
	v_med3_f32 v231, v231, s62, v95
	v_med3_f32 v232, v232, s62, v95
	v_med3_f32 v233, v233, s62, v95
	v_med3_f32 v234, v234, s62, v95
	v_med3_f32 v235, v235, s62, v95
	v_med3_f32 v236, v236, s62, v95
	v_med3_f32 v237, v237, s62, v95
	v_med3_f32 v238, v238, s62, v95
	v_med3_f32 v239, v239, s62, v95
	v_med3_f32 v240, v240, s62, v95
	v_med3_f32 v241, v241, s62, v95
	v_mov_b32_e32 v242, 0
	v_mov_b32_e32 v243, 0
	v_mov_b32_e32 v244, 0
	v_mov_b32_e32 v245, 0
	v_cvt_pk_fp8_f32 v242, v226, v227
	v_cvt_pk_fp8_f32 v243, v230, v231
	v_cvt_pk_fp8_f32 v244, v234, v235
	v_cvt_pk_fp8_f32 v245, v238, v239
	v_cvt_pk_fp8_f32 v242, v228, v229 op_sel:[0,0,1]
	v_cvt_pk_fp8_f32 v243, v232, v233 op_sel:[0,0,1]
	v_cvt_pk_fp8_f32 v244, v236, v237 op_sel:[0,0,1]
	v_cvt_pk_fp8_f32 v245, v240, v241 op_sel:[0,0,1]
	s_nop 0
	global_store_dwordx4 v79, v[242:245], s[6:7]
	ds_read_b32 v226, v214
	ds_read_b32 v227, v214 offset:512
	ds_read_b32 v228, v214 offset:1024
	ds_read_b32 v229, v214 offset:1536
	ds_read_b32 v230, v214 offset:2048
	ds_read_b32 v231, v214 offset:2560
	ds_read_b32 v232, v214 offset:3072
	ds_read_b32 v233, v214 offset:3584
	ds_read_b32 v234, v214 offset:4096
	ds_read_b32 v235, v214 offset:4608
	ds_read_b32 v236, v214 offset:5120
	ds_read_b32 v237, v214 offset:5632
	ds_read_b32 v238, v214 offset:6144
	ds_read_b32 v239, v214 offset:6656
	ds_read_b32 v240, v214 offset:7168
	ds_read_b32 v241, v214 offset:7680
	s_waitcnt lgkmcnt(0)
; #define GAS __attribute__((address_space(1)))
; #define LAS __attribute__((address_space(3)))
; #define LDS_WAIT() asm volatile("s_waitcnt lgkmcnt(0)" ::: "memory")
;     const int pr = item >> 1, kb = 2 * (pr / nblk) + (item & 1), nb = pr % nblk, k0 = 64 * kb, n0 = 32 * nb;
;     const int nr = n0 + (lane & 31); const int sc = MAP == 1 ? src_col_in(nr) : nr;
;     float v[32];
; #pragma unroll
;     for (int i = 0; i < 32; ++i) v[i] = sc >= 0 ? W[(size_t)(k0 + 2 * i + (lane >> 5)) * Nsrc + sc] : 0.f;
; #pragma unroll
;     for (int i = 0; i < 32; ++i) { const int k = k0 + 2 * i + (lane >> 5); float x = v[i] * wscale; if (KS) x *= (k < ksplit ? ksA[k] : ksB[k - ksplit]); scr[(2 * i + (lane >> 5)) * 33 + (lane & 31)] = x; }
;     LDS_WAIT(); asm volatile("" ::: "memory");
;     const int c = lane & 7;
; #pragma unroll
;     for (int j = 0; j < 4; ++j) { const int n = (lane >> 3) + 8 * j; const LAS float* s = scr + (8 * c) * 33 + n;
;         const unsigned long long o = (unsigned long long)pg8::pk4_fp8(s[0 * 33], s[1 * 33], s[2 * 33], s[3 * 33]) | ((unsigned long long)pg8::pk4_fp8(s[4 * 33], s[5 * 33], s[6 * 33], s[7 * 33]) << 32);
;         *(GAS unsigned long long*)(WT + (size_t)(n0 + n) * K + k0 + 8 * c) = o; }
;     LDS_WAIT(); asm volatile("" ::: "memory");
; }
; __global__ void __launch_bounds__(NWAVES * 64, 2) hybrid_fwd(Args args) {
;     ...
;             p0_transpose_item_f8<false>(args.in[16] + (size_t)l * FF * DM, FF, DM, DM / 32, (unsigned char*)(ws + WS_WDN + l * SZ_WDN), 128.f, args.in[16], args.in[16], 0, scr, r, lane);
	v_max_f32_e32 v226, v226, v226
	v_max_f32_e32 v227, v227, v227
	v_max_f32_e32 v228, v228, v228
	v_max_f32_e32 v229, v229, v229
	v_max_f32_e32 v230, v230, v230
	v_max_f32_e32 v231, v231, v231
	v_max_f32_e32 v232, v232, v232
	v_max_f32_e32 v233, v233, v233
	v_max_f32_e32 v234, v234, v234
	v_max_f32_e32 v235, v235, v235
	v_max_f32_e32 v236, v236, v236
	v_max_f32_e32 v237, v237, v237
	v_max_f32_e32 v238, v238, v238
	v_max_f32_e32 v239, v239, v239
	v_max_f32_e32 v240, v240, v240
	v_max_f32_e32 v241, v241, v241
	v_med3_f32 v226, v226, s62, v95
	v_med3_f32 v227, v227, s62, v95
	v_med3_f32 v228, v228, s62, v95
	v_med3_f32 v229, v229, s62, v95
	v_med3_f32 v230, v230, s62, v95
	v_med3_f32 v231, v231, s62, v95
	v_med3_f32 v232, v232, s62, v95
	v_med3_f32 v233, v233, s62, v95
	v_med3_f32 v234, v234, s62, v95
	v_med3_f32 v235, v235, s62, v95
	v_med3_f32 v236, v236, s62, v95
	v_med3_f32 v237, v237, s62, v95
	v_med3_f32 v238, v238, s62, v95
	v_med3_f32 v239, v239, s62, v95
	v_med3_f32 v240, v240, s62, v95
	v_med3_f32 v241, v241, s62, v95
	v_mov_b32_e32 v242, 0
	v_mov_b32_e32 v243, 0
	v_mov_b32_e32 v244, 0
	v_mov_b32_e32 v245, 0
	v_cvt_pk_fp8_f32 v242, v226, v227
	v_cvt_pk_fp8_f32 v243, v230, v231
	v_cvt_pk_fp8_f32 v244, v234, v235
	v_cvt_pk_fp8_f32 v245, v238, v239
	v_cvt_pk_fp8_f32 v242, v228, v229 op_sel:[0,0,1]
	v_cvt_pk_fp8_f32 v243, v232, v233 op_sel:[0,0,1]
	v_cvt_pk_fp8_f32 v244, v236, v237 op_sel:[0,0,1]
	v_cvt_pk_fp8_f32 v245, v240, v241 op_sel:[0,0,1]
	s_nop 0
	global_store_dwordx4 v80, v[242:245], s[6:7]
	s_waitcnt vmcnt(12)
	v_mul_f32_e32 v144, 0x43000000, v144
	v_mul_f32_e32 v145, 0x43000000, v145
	v_mul_f32_e32 v146, 0x43000000, v146
	v_mul_f32_e32 v147, 0x43000000, v147
	ds_write_b128 v209, v[144:147]
	v_mul_f32_e32 v148, 0x43000000, v148
	v_mul_f32_e32 v149, 0x43000000, v149
	v_mul_f32_e32 v150, 0x43000000, v150
	v_mul_f32_e32 v151, 0x43000000, v151
	ds_write_b128 v209, v[148:151] offset:1024
	v_mul_f32_e32 v152, 0x43000000, v152
	v_mul_f32_e32 v153, 0x43000000, v153
	v_mul_f32_e32 v154, 0x43000000, v154
	v_mul_f32_e32 v155, 0x43000000, v155
	ds_write_b128 v209, v[152:155] offset:2048
	v_mul_f32_e32 v156, 0x43000000, v156
	v_mul_f32_e32 v157, 0x43000000, v157
	v_mul_f32_e32 v158, 0x43000000, v158
	v_mul_f32_e32 v159, 0x43000000, v159
	ds_write_b128 v209, v[156:159] offset:3072
	v_mul_f32_e32 v160, 0x43000000, v160
	v_mul_f32_e32 v161, 0x43000000, v161
	v_mul_f32_e32 v162, 0x43000000, v162
	v_mul_f32_e32 v163, 0x43000000, v163
	ds_write_b128 v209, v[160:163] offset:4096
	v_mul_f32_e32 v164, 0x43000000, v164
	v_mul_f32_e32 v165, 0x43000000, v165
	v_mul_f32_e32 v166, 0x43000000, v166
	v_mul_f32_e32 v167, 0x43000000, v167
	ds_write_b128 v209, v[164:167] offset:5120
	v_mul_f32_e32 v168, 0x43000000, v168
	v_mul_f32_e32 v169, 0x43000000, v169
	v_mul_f32_e32 v170, 0x43000000, v170
	v_mul_f32_e32 v171, 0x43000000, v171
	ds_write_b128 v209, v[168:171] offset:6144
	v_mul_f32_e32 v172, 0x43000000, v172
	v_mul_f32_e32 v173, 0x43000000, v173
	v_mul_f32_e32 v174, 0x43000000, v174
	v_mul_f32_e32 v175, 0x43000000, v175
	ds_write_b128 v209, v[172:175] offset:7168
	s_waitcnt lgkmcnt(0)
	s_barrier
	s_add_u32 s8, s38, 0xc000000
	s_addc_u32 s9, s39, 0
	global_load_dwordx4 v[144:147], v75, s[8:9]
	s_add_u32 s8, s8, 0x8000
	s_addc_u32 s9, s9, 0
	global_load_dwordx4 v[148:151], v75, s[8:9]
	s_add_u32 s8, s8, 0x8000
	s_addc_u32 s9, s9, 0
	global_load_dwordx4 v[152:155], v75, s[8:9]
	s_add_u32 s8, s8, 0x8000
	s_addc_u32 s9, s9, 0
	global_load_dwordx4 v[156:159], v75, s[8:9]
	s_add_u32 s8, s8, 0x8000
	s_addc_u32 s9, s9, 0
	global_load_dwordx4 v[160:163], v75, s[8:9]
	s_add_u32 s8, s8, 0x8000
	s_addc_u32 s9, s9, 0
	global_load_dwordx4 v[164:167], v75, s[8:9]
	s_add_u32 s8, s8, 0x8000
	s_addc_u32 s9, s9, 0
	global_load_dwordx4 v[168:171], v75, s[8:9]
	s_add_u32 s8, s8, 0x8000
	s_addc_u32 s9, s9, 0
	global_load_dwordx4 v[172:175], v75, s[8:9]
	s_add_u32 s6, s40, 0x2002000
	s_addc_u32 s7, s41, 0
	ds_read_b32 v226, v211
	ds_read_b32 v227, v211 offset:512
	ds_read_b32 v228, v211 offset:1024
	ds_read_b32 v229, v211 offset:1536
	ds_read_b32 v230, v211 offset:2048
	ds_read_b32 v231, v211 offset:2560
	ds_read_b32 v232, v211 offset:3072
	ds_read_b32 v233, v211 offset:3584
	ds_read_b32 v234, v211 offset:4096
	ds_read_b32 v235, v211 offset:4608
	ds_read_b32 v236, v211 offset:5120
	ds_read_b32 v237, v211 offset:5632
	ds_read_b32 v238, v211 offset:6144
	ds_read_b32 v239, v211 offset:6656
	ds_read_b32 v240, v211 offset:7168
	ds_read_b32 v241, v211 offset:7680
	s_waitcnt lgkmcnt(0)
	v_max_f32_e32 v226, v226, v226
	v_max_f32_e32 v227, v227, v227
	v_max_f32_e32 v228, v228, v228
	v_max_f32_e32 v229, v229, v229
	v_max_f32_e32 v230, v230, v230
	v_max_f32_e32 v231, v231, v231
	v_max_f32_e32 v232, v232, v232
	v_max_f32_e32 v233, v233, v233
	v_max_f32_e32 v234, v234, v234
	v_max_f32_e32 v235, v235, v235
	v_max_f32_e32 v236, v236, v236
	v_max_f32_e32 v237, v237, v237
	v_max_f32_e32 v238, v238, v238
	v_max_f32_e32 v239, v239, v239
	v_max_f32_e32 v240, v240, v240
	v_max_f32_e32 v241, v241, v241
	v_med3_f32 v226, v226, s62, v95
	v_med3_f32 v227, v227, s62, v95
	v_med3_f32 v228, v228, s62, v95
	v_med3_f32 v229, v229, s62, v95
	v_med3_f32 v230, v230, s62, v95
	v_med3_f32 v231, v231, s62, v95
	v_med3_f32 v232, v232, s62, v95
	v_med3_f32 v233, v233, s62, v95
	v_med3_f32 v234, v234, s62, v95
	v_med3_f32 v235, v235, s62, v95
	v_med3_f32 v236, v236, s62, v95
	v_med3_f32 v237, v237, s62, v95
	v_med3_f32 v238, v238, s62, v95
	v_med3_f32 v239, v239, s62, v95
	v_med3_f32 v240, v240, s62, v95
	v_med3_f32 v241, v241, s62, v95
	v_mov_b32_e32 v242, 0
	v_mov_b32_e32 v243, 0
	v_mov_b32_e32 v244, 0
	v_mov_b32_e32 v245, 0
	v_cvt_pk_fp8_f32 v242, v226, v227
	v_cvt_pk_fp8_f32 v243, v230, v231
	v_cvt_pk_fp8_f32 v244, v234, v235
	v_cvt_pk_fp8_f32 v245, v238, v239
	v_cvt_pk_fp8_f32 v242, v228, v229 op_sel:[0,0,1]
	v_cvt_pk_fp8_f32 v243, v232, v233 op_sel:[0,0,1]
	v_cvt_pk_fp8_f32 v244, v236, v237 op_sel:[0,0,1]
	v_cvt_pk_fp8_f32 v245, v240, v241 op_sel:[0,0,1]
	s_nop 0
	global_store_dwordx4 v79, v[242:245], s[6:7]
	ds_read_b32 v226, v213
	ds_read_b32 v227, v213 offset:512
	ds_read_b32 v228, v213 offset:1024
	ds_read_b32 v229, v213 offset:1536
	ds_read_b32 v230, v213 offset:2048
	ds_read_b32 v231, v213 offset:2560
	ds_read_b32 v232, v213 offset:3072
	ds_read_b32 v233, v213 offset:3584
	ds_read_b32 v234, v213 offset:4096
	ds_read_b32 v235, v213 offset:4608
	ds_read_b32 v236, v213 offset:5120
	ds_read_b32 v237, v213 offset:5632
	ds_read_b32 v238, v213 offset:6144
	ds_read_b32 v239, v213 offset:6656
	ds_read_b32 v240, v213 offset:7168
	ds_read_b32 v241, v213 offset:7680
	s_waitcnt lgkmcnt(0)
; #define GAS __attribute__((address_space(1)))
; #define LAS __attribute__((address_space(3)))
; #define LDS_WAIT() asm volatile("s_waitcnt lgkmcnt(0)" ::: "memory")
;     const int pr = item >> 1, kb = 2 * (pr / nblk) + (item & 1), nb = pr % nblk, k0 = 64 * kb, n0 = 32 * nb;
;     const int nr = n0 + (lane & 31); const int sc = MAP == 1 ? src_col_in(nr) : nr;
;     float v[32];
; #pragma unroll
;     for (int i = 0; i < 32; ++i) v[i] = sc >= 0 ? W[(size_t)(k0 + 2 * i + (lane >> 5)) * Nsrc + sc] : 0.f;
; #pragma unroll
;     for (int i = 0; i < 32; ++i) { const int k = k0 + 2 * i + (lane >> 5); float x = v[i] * wscale; if (KS) x *= (k < ksplit ? ksA[k] : ksB[k - ksplit]); scr[(2 * i + (lane >> 5)) * 33 + (lane & 31)] = x; }
;     LDS_WAIT(); asm volatile("" ::: "memory");
;     const int c = lane & 7;
; #pragma unroll
;     for (int j = 0; j < 4; ++j) { const int n = (lane >> 3) + 8 * j; const LAS float* s = scr + (8 * c) * 33 + n;
;         const unsigned long long o = (unsigned long long)pg8::pk4_fp8(s[0 * 33], s[1 * 33], s[2 * 33], s[3 * 33]) | ((unsigned long long)pg8::pk4_fp8(s[4 * 33], s[5 * 33], s[6 * 33], s[7 * 33]) << 32);
;         *(GAS unsigned long long*)(WT + (size_t)(n0 + n) * K + k0 + 8 * c) = o; }
;     LDS_WAIT(); asm volatile("" ::: "memory");
; }
; __global__ void __launch_bounds__(NWAVES * 64, 2) hybrid_fwd(Args args) {
;     ...
;             p0_transpose_item_f8<false>(args.in[16] + (size_t)l * FF * DM, FF, DM, DM / 32, (unsigned char*)(ws + WS_WDN + l * SZ_WDN), 128.f, args.in[16], args.in[16], 0, scr, r, lane);
	v_max_f32_e32 v226, v226, v226
	v_max_f32_e32 v227, v227, v227
	v_max_f32_e32 v228, v228, v228
	v_max_f32_e32 v229, v229, v229
	v_max_f32_e32 v230, v230, v230
	v_max_f32_e32 v231, v231, v231
	v_max_f32_e32 v232, v232, v232
	v_max_f32_e32 v233, v233, v233
	v_max_f32_e32 v234, v234, v234
	v_max_f32_e32 v235, v235, v235
	v_max_f32_e32 v236, v236, v236
	v_max_f32_e32 v237, v237, v237
	v_max_f32_e32 v238, v238, v238
	v_max_f32_e32 v239, v239, v239
	v_max_f32_e32 v240, v240, v240
	v_max_f32_e32 v241, v241, v241
	v_med3_f32 v226, v226, s62, v95
	v_med3_f32 v227, v227, s62, v95
	v_med3_f32 v228, v228, s62, v95
	v_med3_f32 v229, v229, s62, v95
	v_med3_f32 v230, v230, s62, v95
	v_med3_f32 v231, v231, s62, v95
	v_med3_f32 v232, v232, s62, v95
	v_med3_f32 v233, v233, s62, v95
	v_med3_f32 v234, v234, s62, v95
	v_med3_f32 v235, v235, s62, v95
	v_med3_f32 v236, v236, s62, v95
	v_med3_f32 v237, v237, s62, v95
	v_med3_f32 v238, v238, s62, v95
	v_med3_f32 v239, v239, s62, v95
	v_med3_f32 v240, v240, s62, v95
	v_med3_f32 v241, v241, s62, v95
	v_mov_b32_e32 v242, 0
	v_mov_b32_e32 v243, 0
	v_mov_b32_e32 v244, 0
	v_mov_b32_e32 v245, 0
	v_cvt_pk_fp8_f32 v242, v226, v227
	v_cvt_pk_fp8_f32 v243, v230, v231
	v_cvt_pk_fp8_f32 v244, v234, v235
	v_cvt_pk_fp8_f32 v245, v238, v239
	v_cvt_pk_fp8_f32 v242, v228, v229 op_sel:[0,0,1]
	v_cvt_pk_fp8_f32 v243, v232, v233 op_sel:[0,0,1]
	v_cvt_pk_fp8_f32 v244, v236, v237 op_sel:[0,0,1]
	v_cvt_pk_fp8_f32 v245, v240, v241 op_sel:[0,0,1]
	s_nop 0
	global_store_dwordx4 v80, v[242:245], s[6:7]
	s_waitcnt vmcnt(12)
	v_mul_f32_e32 v176, 0x43000000, v176
	v_mul_f32_e32 v177, 0x43000000, v177
	v_mul_f32_e32 v178, 0x43000000, v178
	v_mul_f32_e32 v179, 0x43000000, v179
	ds_write_b128 v210, v[176:179]
	v_mul_f32_e32 v180, 0x43000000, v180
	v_mul_f32_e32 v181, 0x43000000, v181
	v_mul_f32_e32 v182, 0x43000000, v182
	v_mul_f32_e32 v183, 0x43000000, v183
	ds_write_b128 v210, v[180:183] offset:1024
	v_mul_f32_e32 v184, 0x43000000, v184
	v_mul_f32_e32 v185, 0x43000000, v185
	v_mul_f32_e32 v186, 0x43000000, v186
	v_mul_f32_e32 v187, 0x43000000, v187
	ds_write_b128 v210, v[184:187] offset:2048
	v_mul_f32_e32 v188, 0x43000000, v188
	v_mul_f32_e32 v189, 0x43000000, v189
	v_mul_f32_e32 v190, 0x43000000, v190
	v_mul_f32_e32 v191, 0x43000000, v191
	ds_write_b128 v210, v[188:191] offset:3072
	v_mul_f32_e32 v192, 0x43000000, v192
	v_mul_f32_e32 v193, 0x43000000, v193
	v_mul_f32_e32 v194, 0x43000000, v194
	v_mul_f32_e32 v195, 0x43000000, v195
	ds_write_b128 v210, v[192:195] offset:4096
	v_mul_f32_e32 v196, 0x43000000, v196
	v_mul_f32_e32 v197, 0x43000000, v197
	v_mul_f32_e32 v198, 0x43000000, v198
	v_mul_f32_e32 v199, 0x43000000, v199
	ds_write_b128 v210, v[196:199] offset:5120
	v_mul_f32_e32 v200, 0x43000000, v200
	v_mul_f32_e32 v201, 0x43000000, v201
	v_mul_f32_e32 v202, 0x43000000, v202
	v_mul_f32_e32 v203, 0x43000000, v203
	ds_write_b128 v210, v[200:203] offset:6144
	v_mul_f32_e32 v204, 0x43000000, v204
	v_mul_f32_e32 v205, 0x43000000, v205
	v_mul_f32_e32 v206, 0x43000000, v206
	v_mul_f32_e32 v207, 0x43000000, v207
	ds_write_b128 v210, v[204:207] offset:7168
	s_waitcnt lgkmcnt(0)
	s_barrier
	s_add_u32 s8, s38, 0xc001000
	s_addc_u32 s9, s39, 0
	global_load_dwordx4 v[176:179], v75, s[8:9]
	s_add_u32 s8, s8, 0x8000
	s_addc_u32 s9, s9, 0
	global_load_dwordx4 v[180:183], v75, s[8:9]
	s_add_u32 s8, s8, 0x8000
	s_addc_u32 s9, s9, 0
	global_load_dwordx4 v[184:187], v75, s[8:9]
	s_add_u32 s8, s8, 0x8000
	s_addc_u32 s9, s9, 0
	global_load_dwordx4 v[188:191], v75, s[8:9]
	s_add_u32 s8, s8, 0x8000
	s_addc_u32 s9, s9, 0
	global_load_dwordx4 v[192:195], v75, s[8:9]
	s_add_u32 s8, s8, 0x8000
	s_addc_u32 s9, s9, 0
	global_load_dwordx4 v[196:199], v75, s[8:9]
	s_add_u32 s8, s8, 0x8000
	s_addc_u32 s9, s9, 0
	global_load_dwordx4 v[200:203], v75, s[8:9]
	s_add_u32 s8, s8, 0x8000
	s_addc_u32 s9, s9, 0
	global_load_dwordx4 v[204:207], v75, s[8:9]
	s_add_u32 s6, s40, 0x3002000
	s_addc_u32 s7, s41, 0
	ds_read_b32 v226, v212
	ds_read_b32 v227, v212 offset:512
	ds_read_b32 v228, v212 offset:1024
	ds_read_b32 v229, v212 offset:1536
	ds_read_b32 v230, v212 offset:2048
	ds_read_b32 v231, v212 offset:2560
	ds_read_b32 v232, v212 offset:3072
	ds_read_b32 v233, v212 offset:3584
	ds_read_b32 v234, v212 offset:4096
	ds_read_b32 v235, v212 offset:4608
	ds_read_b32 v236, v212 offset:5120
	ds_read_b32 v237, v212 offset:5632
	ds_read_b32 v238, v212 offset:6144
	ds_read_b32 v239, v212 offset:6656
	ds_read_b32 v240, v212 offset:7168
	ds_read_b32 v241, v212 offset:7680
	s_waitcnt lgkmcnt(0)
	v_max_f32_e32 v226, v226, v226
	v_max_f32_e32 v227, v227, v227
	v_max_f32_e32 v228, v228, v228
	v_max_f32_e32 v229, v229, v229
	v_max_f32_e32 v230, v230, v230
	v_max_f32_e32 v231, v231, v231
	v_max_f32_e32 v232, v232, v232
	v_max_f32_e32 v233, v233, v233
	v_max_f32_e32 v234, v234, v234
	v_max_f32_e32 v235, v235, v235
	v_max_f32_e32 v236, v236, v236
	v_max_f32_e32 v237, v237, v237
	v_max_f32_e32 v238, v238, v238
	v_max_f32_e32 v239, v239, v239
	v_max_f32_e32 v240, v240, v240
	v_max_f32_e32 v241, v241, v241
	v_med3_f32 v226, v226, s62, v95
	v_med3_f32 v227, v227, s62, v95
	v_med3_f32 v228, v228, s62, v95
	v_med3_f32 v229, v229, s62, v95
	v_med3_f32 v230, v230, s62, v95
	v_med3_f32 v231, v231, s62, v95
	v_med3_f32 v232, v232, s62, v95
	v_med3_f32 v233, v233, s62, v95
	v_med3_f32 v234, v234, s62, v95
	v_med3_f32 v235, v235, s62, v95
	v_med3_f32 v236, v236, s62, v95
	v_med3_f32 v237, v237, s62, v95
	v_med3_f32 v238, v238, s62, v95
	v_med3_f32 v239, v239, s62, v95
	v_med3_f32 v240, v240, s62, v95
	v_med3_f32 v241, v241, s62, v95
	v_mov_b32_e32 v242, 0
	v_mov_b32_e32 v243, 0
	v_mov_b32_e32 v244, 0
	v_mov_b32_e32 v245, 0
	v_cvt_pk_fp8_f32 v242, v226, v227
	v_cvt_pk_fp8_f32 v243, v230, v231
	v_cvt_pk_fp8_f32 v244, v234, v235
	v_cvt_pk_fp8_f32 v245, v238, v239
	v_cvt_pk_fp8_f32 v242, v228, v229 op_sel:[0,0,1]
	v_cvt_pk_fp8_f32 v243, v232, v233 op_sel:[0,0,1]
	v_cvt_pk_fp8_f32 v244, v236, v237 op_sel:[0,0,1]
	v_cvt_pk_fp8_f32 v245, v240, v241 op_sel:[0,0,1]
	s_nop 0
	global_store_dwordx4 v79, v[242:245], s[6:7]
	ds_read_b32 v226, v214
	ds_read_b32 v227, v214 offset:512
	ds_read_b32 v228, v214 offset:1024
	ds_read_b32 v229, v214 offset:1536
	ds_read_b32 v230, v214 offset:2048
	ds_read_b32 v231, v214 offset:2560
	ds_read_b32 v232, v214 offset:3072
	ds_read_b32 v233, v214 offset:3584
	ds_read_b32 v234, v214 offset:4096
	ds_read_b32 v235, v214 offset:4608
	ds_read_b32 v236, v214 offset:5120
	ds_read_b32 v237, v214 offset:5632
	ds_read_b32 v238, v214 offset:6144
	ds_read_b32 v239, v214 offset:6656
	ds_read_b32 v240, v214 offset:7168
	ds_read_b32 v241, v214 offset:7680
	s_waitcnt lgkmcnt(0)
; #define GAS __attribute__((address_space(1)))
; #define LAS __attribute__((address_space(3)))
; #define LDS_WAIT() asm volatile("s_waitcnt lgkmcnt(0)" ::: "memory")
;     const int pr = item >> 1, kb = 2 * (pr / nblk) + (item & 1), nb = pr % nblk, k0 = 64 * kb, n0 = 32 * nb;
;     const int nr = n0 + (lane & 31); const int sc = MAP == 1 ? src_col_in(nr) : nr;
;     float v[32];
; #pragma unroll
;     for (int i = 0; i < 32; ++i) v[i] = sc >= 0 ? W[(size_t)(k0 + 2 * i + (lane >> 5)) * Nsrc + sc] : 0.f;
; #pragma unroll
;     for (int i = 0; i < 32; ++i) { const int k = k0 + 2 * i + (lane >> 5); float x = v[i] * wscale; if (KS) x *= (k < ksplit ? ksA[k] : ksB[k - ksplit]); scr[(2 * i + (lane >> 5)) * 33 + (lane & 31)] = x; }
;     LDS_WAIT(); asm volatile("" ::: "memory");
;     const int c = lane & 7;
; #pragma unroll
;     for (int j = 0; j < 4; ++j) { const int n = (lane >> 3) + 8 * j; const LAS float* s = scr + (8 * c) * 33 + n;
;         const unsigned long long o = (unsigned long long)pg8::pk4_fp8(s[0 * 33], s[1 * 33], s[2 * 33], s[3 * 33]) | ((unsigned long long)pg8::pk4_fp8(s[4 * 33], s[5 * 33], s[6 * 33], s[7 * 33]) << 32);
;         *(GAS unsigned long long*)(WT + (size_t)(n0 + n) * K + k0 + 8 * c) = o; }
;     LDS_WAIT(); asm volatile("" ::: "memory");
; }
; __global__ void __launch_bounds__(NWAVES * 64, 2) hybrid_fwd(Args args) {
;     ...
;             p0_transpose_item_f8<false>(args.in[16] + (size_t)l * FF * DM, FF, DM, DM / 32, (unsigned char*)(ws + WS_WDN + l * SZ_WDN), 128.f, args.in[16], args.in[16], 0, scr, r, lane);
	v_max_f32_e32 v226, v226, v226
	v_max_f32_e32 v227, v227, v227
	v_max_f32_e32 v228, v228, v228
	v_max_f32_e32 v229, v229, v229
	v_max_f32_e32 v230, v230, v230
	v_max_f32_e32 v231, v231, v231
	v_max_f32_e32 v232, v232, v232
	v_max_f32_e32 v233, v233, v233
	v_max_f32_e32 v234, v234, v234
	v_max_f32_e32 v235, v235, v235
	v_max_f32_e32 v236, v236, v236
	v_max_f32_e32 v237, v237, v237
	v_max_f32_e32 v238, v238, v238
	v_max_f32_e32 v239, v239, v239
	v_max_f32_e32 v240, v240, v240
	v_max_f32_e32 v241, v241, v241
	v_med3_f32 v226, v226, s62, v95
	v_med3_f32 v227, v227, s62, v95
	v_med3_f32 v228, v228, s62, v95
	v_med3_f32 v229, v229, s62, v95
	v_med3_f32 v230, v230, s62, v95
	v_med3_f32 v231, v231, s62, v95
	v_med3_f32 v232, v232, s62, v95
	v_med3_f32 v233, v233, s62, v95
	v_med3_f32 v234, v234, s62, v95
	v_med3_f32 v235, v235, s62, v95
	v_med3_f32 v236, v236, s62, v95
	v_med3_f32 v237, v237, s62, v95
	v_med3_f32 v238, v238, s62, v95
	v_med3_f32 v239, v239, s62, v95
	v_med3_f32 v240, v240, s62, v95
	v_med3_f32 v241, v241, s62, v95
	v_mov_b32_e32 v242, 0
	v_mov_b32_e32 v243, 0
	v_mov_b32_e32 v244, 0
	v_mov_b32_e32 v245, 0
	v_cvt_pk_fp8_f32 v242, v226, v227
	v_cvt_pk_fp8_f32 v243, v230, v231
	v_cvt_pk_fp8_f32 v244, v234, v235
	v_cvt_pk_fp8_f32 v245, v238, v239
	v_cvt_pk_fp8_f32 v242, v228, v229 op_sel:[0,0,1]
	v_cvt_pk_fp8_f32 v243, v232, v233 op_sel:[0,0,1]
	v_cvt_pk_fp8_f32 v244, v236, v237 op_sel:[0,0,1]
	v_cvt_pk_fp8_f32 v245, v240, v241 op_sel:[0,0,1]
	s_nop 0
	global_store_dwordx4 v80, v[242:245], s[6:7]
	s_waitcnt vmcnt(12)
	v_mul_f32_e32 v144, 0x43000000, v144
	v_mul_f32_e32 v145, 0x43000000, v145
	v_mul_f32_e32 v146, 0x43000000, v146
	v_mul_f32_e32 v147, 0x43000000, v147
	ds_write_b128 v209, v[144:147]
	v_mul_f32_e32 v148, 0x43000000, v148
	v_mul_f32_e32 v149, 0x43000000, v149
	v_mul_f32_e32 v150, 0x43000000, v150
	v_mul_f32_e32 v151, 0x43000000, v151
	ds_write_b128 v209, v[148:151] offset:1024
	v_mul_f32_e32 v152, 0x43000000, v152
	v_mul_f32_e32 v153, 0x43000000, v153
	v_mul_f32_e32 v154, 0x43000000, v154
	v_mul_f32_e32 v155, 0x43000000, v155
	ds_write_b128 v209, v[152:155] offset:2048
	v_mul_f32_e32 v156, 0x43000000, v156
	v_mul_f32_e32 v157, 0x43000000, v157
	v_mul_f32_e32 v158, 0x43000000, v158
	v_mul_f32_e32 v159, 0x43000000, v159
	ds_write_b128 v209, v[156:159] offset:3072
	v_mul_f32_e32 v160, 0x43000000, v160
	v_mul_f32_e32 v161, 0x43000000, v161
	v_mul_f32_e32 v162, 0x43000000, v162
	v_mul_f32_e32 v163, 0x43000000, v163
	ds_write_b128 v209, v[160:163] offset:4096
	v_mul_f32_e32 v164, 0x43000000, v164
	v_mul_f32_e32 v165, 0x43000000, v165
	v_mul_f32_e32 v166, 0x43000000, v166
	v_mul_f32_e32 v167, 0x43000000, v167
	ds_write_b128 v209, v[164:167] offset:5120
	v_mul_f32_e32 v168, 0x43000000, v168
	v_mul_f32_e32 v169, 0x43000000, v169
	v_mul_f32_e32 v170, 0x43000000, v170
	v_mul_f32_e32 v171, 0x43000000, v171
	ds_write_b128 v209, v[168:171] offset:6144
	v_mul_f32_e32 v172, 0x43000000, v172
	v_mul_f32_e32 v173, 0x43000000, v173
	v_mul_f32_e32 v174, 0x43000000, v174
	v_mul_f32_e32 v175, 0x43000000, v175
	ds_write_b128 v209, v[172:175] offset:7168
	s_waitcnt lgkmcnt(0)
	s_barrier
	s_add_u32 s8, s38, 0xc002000
	s_addc_u32 s9, s39, 0
	global_load_dwordx4 v[144:147], v75, s[8:9]
	s_add_u32 s8, s8, 0x8000
	s_addc_u32 s9, s9, 0
	global_load_dwordx4 v[148:151], v75, s[8:9]
	s_add_u32 s8, s8, 0x8000
	s_addc_u32 s9, s9, 0
	global_load_dwordx4 v[152:155], v75, s[8:9]
	s_add_u32 s8, s8, 0x8000
	s_addc_u32 s9, s9, 0
	global_load_dwordx4 v[156:159], v75, s[8:9]
	s_add_u32 s8, s8, 0x8000
	s_addc_u32 s9, s9, 0
	global_load_dwordx4 v[160:163], v75, s[8:9]
	s_add_u32 s8, s8, 0x8000
	s_addc_u32 s9, s9, 0
	global_load_dwordx4 v[164:167], v75, s[8:9]
	s_add_u32 s8, s8, 0x8000
	s_addc_u32 s9, s9, 0
	global_load_dwordx4 v[168:171], v75, s[8:9]
	s_add_u32 s8, s8, 0x8000
	s_addc_u32 s9, s9, 0
	global_load_dwordx4 v[172:175], v75, s[8:9]
	s_add_u32 s6, s40, 0x3000
	s_addc_u32 s7, s41, 0
	ds_read_b32 v226, v211
	ds_read_b32 v227, v211 offset:512
	ds_read_b32 v228, v211 offset:1024
	ds_read_b32 v229, v211 offset:1536
	ds_read_b32 v230, v211 offset:2048
	ds_read_b32 v231, v211 offset:2560
	ds_read_b32 v232, v211 offset:3072
	ds_read_b32 v233, v211 offset:3584
	ds_read_b32 v234, v211 offset:4096
	ds_read_b32 v235, v211 offset:4608
	ds_read_b32 v236, v211 offset:5120
	ds_read_b32 v237, v211 offset:5632
	ds_read_b32 v238, v211 offset:6144
	ds_read_b32 v239, v211 offset:6656
	ds_read_b32 v240, v211 offset:7168
	ds_read_b32 v241, v211 offset:7680
	s_waitcnt lgkmcnt(0)
	v_max_f32_e32 v226, v226, v226
	v_max_f32_e32 v227, v227, v227
	v_max_f32_e32 v228, v228, v228
	v_max_f32_e32 v229, v229, v229
	v_max_f32_e32 v230, v230, v230
	v_max_f32_e32 v231, v231, v231
	v_max_f32_e32 v232, v232, v232
	v_max_f32_e32 v233, v233, v233
	v_max_f32_e32 v234, v234, v234
	v_max_f32_e32 v235, v235, v235
	v_max_f32_e32 v236, v236, v236
	v_max_f32_e32 v237, v237, v237
	v_max_f32_e32 v238, v238, v238
	v_max_f32_e32 v239, v239, v239
	v_max_f32_e32 v240, v240, v240
	v_max_f32_e32 v241, v241, v241
	v_med3_f32 v226, v226, s62, v95
	v_med3_f32 v227, v227, s62, v95
	v_med3_f32 v228, v228, s62, v95
	v_med3_f32 v229, v229, s62, v95
	v_med3_f32 v230, v230, s62, v95
	v_med3_f32 v231, v231, s62, v95
	v_med3_f32 v232, v232, s62, v95
	v_med3_f32 v233, v233, s62, v95
	v_med3_f32 v234, v234, s62, v95
	v_med3_f32 v235, v235, s62, v95
	v_med3_f32 v236, v236, s62, v95
	v_med3_f32 v237, v237, s62, v95
	v_med3_f32 v238, v238, s62, v95
	v_med3_f32 v239, v239, s62, v95
	v_med3_f32 v240, v240, s62, v95
	v_med3_f32 v241, v241, s62, v95
	v_mov_b32_e32 v242, 0
	v_mov_b32_e32 v243, 0
	v_mov_b32_e32 v244, 0
	v_mov_b32_e32 v245, 0
	v_cvt_pk_fp8_f32 v242, v226, v227
	v_cvt_pk_fp8_f32 v243, v230, v231
	v_cvt_pk_fp8_f32 v244, v234, v235
	v_cvt_pk_fp8_f32 v245, v238, v239
	v_cvt_pk_fp8_f32 v242, v228, v229 op_sel:[0,0,1]
	v_cvt_pk_fp8_f32 v243, v232, v233 op_sel:[0,0,1]
	v_cvt_pk_fp8_f32 v244, v236, v237 op_sel:[0,0,1]
	v_cvt_pk_fp8_f32 v245, v240, v241 op_sel:[0,0,1]
	s_nop 0
	global_store_dwordx4 v79, v[242:245], s[6:7]
	ds_read_b32 v226, v213
	ds_read_b32 v227, v213 offset:512
	ds_read_b32 v228, v213 offset:1024
	ds_read_b32 v229, v213 offset:1536
	ds_read_b32 v230, v213 offset:2048
	ds_read_b32 v231, v213 offset:2560
	ds_read_b32 v232, v213 offset:3072
	ds_read_b32 v233, v213 offset:3584
	ds_read_b32 v234, v213 offset:4096
	ds_read_b32 v235, v213 offset:4608
	ds_read_b32 v236, v213 offset:5120
	ds_read_b32 v237, v213 offset:5632
	ds_read_b32 v238, v213 offset:6144
	ds_read_b32 v239, v213 offset:6656
	ds_read_b32 v240, v213 offset:7168
	ds_read_b32 v241, v213 offset:7680
	s_waitcnt lgkmcnt(0)
; #define GAS __attribute__((address_space(1)))
; #define LAS __attribute__((address_space(3)))
; #define LDS_WAIT() asm volatile("s_waitcnt lgkmcnt(0)" ::: "memory")
;     const int pr = item >> 1, kb = 2 * (pr / nblk) + (item & 1), nb = pr % nblk, k0 = 64 * kb, n0 = 32 * nb;
;     const int nr = n0 + (lane & 31); const int sc = MAP == 1 ? src_col_in(nr) : nr;
;     float v[32];
; #pragma unroll
;     for (int i = 0; i < 32; ++i) v[i] = sc >= 0 ? W[(size_t)(k0 + 2 * i + (lane >> 5)) * Nsrc + sc] : 0.f;
; #pragma unroll
;     for (int i = 0; i < 32; ++i) { const int k = k0 + 2 * i + (lane >> 5); float x = v[i] * wscale; if (KS) x *= (k < ksplit ? ksA[k] : ksB[k - ksplit]); scr[(2 * i + (lane >> 5)) * 33 + (lane & 31)] = x; }
;     LDS_WAIT(); asm volatile("" ::: "memory");
;     const int c = lane & 7;
; #pragma unroll
;     for (int j = 0; j < 4; ++j) { const int n = (lane >> 3) + 8 * j; const LAS float* s = scr + (8 * c) * 33 + n;
;         const unsigned long long o = (unsigned long long)pg8::pk4_fp8(s[0 * 33], s[1 * 33], s[2 * 33], s[3 * 33]) | ((unsigned long long)pg8::pk4_fp8(s[4 * 33], s[5 * 33], s[6 * 33], s[7 * 33]) << 32);
;         *(GAS unsigned long long*)(WT + (size_t)(n0 + n) * K + k0 + 8 * c) = o; }
;     LDS_WAIT(); asm volatile("" ::: "memory");
; }
; __global__ void __launch_bounds__(NWAVES * 64, 2) hybrid_fwd(Args args) {
;     ...
;             p0_transpose_item_f8<false>(args.in[16] + (size_t)l * FF * DM, FF, DM, DM / 32, (unsigned char*)(ws + WS_WDN + l * SZ_WDN), 128.f, args.in[16], args.in[16], 0, scr, r, lane);
	v_max_f32_e32 v226, v226, v226
	v_max_f32_e32 v227, v227, v227
	v_max_f32_e32 v228, v228, v228
	v_max_f32_e32 v229, v229, v229
	v_max_f32_e32 v230, v230, v230
	v_max_f32_e32 v231, v231, v231
	v_max_f32_e32 v232, v232, v232
	v_max_f32_e32 v233, v233, v233
	v_max_f32_e32 v234, v234, v234
	v_max_f32_e32 v235, v235, v235
	v_max_f32_e32 v236, v236, v236
	v_max_f32_e32 v237, v237, v237
	v_max_f32_e32 v238, v238, v238
	v_max_f32_e32 v239, v239, v239
	v_max_f32_e32 v240, v240, v240
	v_max_f32_e32 v241, v241, v241
	v_med3_f32 v226, v226, s62, v95
	v_med3_f32 v227, v227, s62, v95
	v_med3_f32 v228, v228, s62, v95
	v_med3_f32 v229, v229, s62, v95
	v_med3_f32 v230, v230, s62, v95
	v_med3_f32 v231, v231, s62, v95
	v_med3_f32 v232, v232, s62, v95
	v_med3_f32 v233, v233, s62, v95
	v_med3_f32 v234, v234, s62, v95
	v_med3_f32 v235, v235, s62, v95
	v_med3_f32 v236, v236, s62, v95
	v_med3_f32 v237, v237, s62, v95
	v_med3_f32 v238, v238, s62, v95
	v_med3_f32 v239, v239, s62, v95
	v_med3_f32 v240, v240, s62, v95
	v_med3_f32 v241, v241, s62, v95
	v_mov_b32_e32 v242, 0
	v_mov_b32_e32 v243, 0
	v_mov_b32_e32 v244, 0
	v_mov_b32_e32 v245, 0
	v_cvt_pk_fp8_f32 v242, v226, v227
	v_cvt_pk_fp8_f32 v243, v230, v231
	v_cvt_pk_fp8_f32 v244, v234, v235
	v_cvt_pk_fp8_f32 v245, v238, v239
	v_cvt_pk_fp8_f32 v242, v228, v229 op_sel:[0,0,1]
	v_cvt_pk_fp8_f32 v243, v232, v233 op_sel:[0,0,1]
	v_cvt_pk_fp8_f32 v244, v236, v237 op_sel:[0,0,1]
	v_cvt_pk_fp8_f32 v245, v240, v241 op_sel:[0,0,1]
	s_nop 0
	global_store_dwordx4 v80, v[242:245], s[6:7]
	s_waitcnt vmcnt(12)
	v_mul_f32_e32 v176, 0x43000000, v176
	v_mul_f32_e32 v177, 0x43000000, v177
	v_mul_f32_e32 v178, 0x43000000, v178
	v_mul_f32_e32 v179, 0x43000000, v179
	ds_write_b128 v210, v[176:179]
	v_mul_f32_e32 v180, 0x43000000, v180
	v_mul_f32_e32 v181, 0x43000000, v181
	v_mul_f32_e32 v182, 0x43000000, v182
	v_mul_f32_e32 v183, 0x43000000, v183
	ds_write_b128 v210, v[180:183] offset:1024
	v_mul_f32_e32 v184, 0x43000000, v184
	v_mul_f32_e32 v185, 0x43000000, v185
	v_mul_f32_e32 v186, 0x43000000, v186
	v_mul_f32_e32 v187, 0x43000000, v187
	ds_write_b128 v210, v[184:187] offset:2048
	v_mul_f32_e32 v188, 0x43000000, v188
	v_mul_f32_e32 v189, 0x43000000, v189
	v_mul_f32_e32 v190, 0x43000000, v190
	v_mul_f32_e32 v191, 0x43000000, v191
	ds_write_b128 v210, v[188:191] offset:3072
	v_mul_f32_e32 v192, 0x43000000, v192
	v_mul_f32_e32 v193, 0x43000000, v193
	v_mul_f32_e32 v194, 0x43000000, v194
	v_mul_f32_e32 v195, 0x43000000, v195
	ds_write_b128 v210, v[192:195] offset:4096
	v_mul_f32_e32 v196, 0x43000000, v196
	v_mul_f32_e32 v197, 0x43000000, v197
	v_mul_f32_e32 v198, 0x43000000, v198
	v_mul_f32_e32 v199, 0x43000000, v199
	ds_write_b128 v210, v[196:199] offset:5120
	v_mul_f32_e32 v200, 0x43000000, v200
	v_mul_f32_e32 v201, 0x43000000, v201
	v_mul_f32_e32 v202, 0x43000000, v202
	v_mul_f32_e32 v203, 0x43000000, v203
	ds_write_b128 v210, v[200:203] offset:6144
	v_mul_f32_e32 v204, 0x43000000, v204
	v_mul_f32_e32 v205, 0x43000000, v205
	v_mul_f32_e32 v206, 0x43000000, v206
	v_mul_f32_e32 v207, 0x43000000, v207
	ds_write_b128 v210, v[204:207] offset:7168
	s_waitcnt lgkmcnt(0)
	s_barrier
	s_add_u32 s8, s38, 0xc003000
	s_addc_u32 s9, s39, 0
	global_load_dwordx4 v[176:179], v75, s[8:9]
	s_add_u32 s8, s8, 0x8000
	s_addc_u32 s9, s9, 0
	global_load_dwordx4 v[180:183], v75, s[8:9]
	s_add_u32 s8, s8, 0x8000
	s_addc_u32 s9, s9, 0
	global_load_dwordx4 v[184:187], v75, s[8:9]
	s_add_u32 s8, s8, 0x8000
	s_addc_u32 s9, s9, 0
	global_load_dwordx4 v[188:191], v75, s[8:9]
	s_add_u32 s8, s8, 0x8000
	s_addc_u32 s9, s9, 0
	global_load_dwordx4 v[192:195], v75, s[8:9]
	s_add_u32 s8, s8, 0x8000
	s_addc_u32 s9, s9, 0
	global_load_dwordx4 v[196:199], v75, s[8:9]
	s_add_u32 s8, s8, 0x8000
	s_addc_u32 s9, s9, 0
	global_load_dwordx4 v[200:203], v75, s[8:9]
	s_add_u32 s8, s8, 0x8000
	s_addc_u32 s9, s9, 0
	global_load_dwordx4 v[204:207], v75, s[8:9]
	s_add_u32 s6, s40, 0x1003000
	s_addc_u32 s7, s41, 0
	ds_read_b32 v226, v212
	ds_read_b32 v227, v212 offset:512
	ds_read_b32 v228, v212 offset:1024
	ds_read_b32 v229, v212 offset:1536
	ds_read_b32 v230, v212 offset:2048
	ds_read_b32 v231, v212 offset:2560
	ds_read_b32 v232, v212 offset:3072
	ds_read_b32 v233, v212 offset:3584
	ds_read_b32 v234, v212 offset:4096
	ds_read_b32 v235, v212 offset:4608
	ds_read_b32 v236, v212 offset:5120
	ds_read_b32 v237, v212 offset:5632
	ds_read_b32 v238, v212 offset:6144
	ds_read_b32 v239, v212 offset:6656
	ds_read_b32 v240, v212 offset:7168
	ds_read_b32 v241, v212 offset:7680
	s_waitcnt lgkmcnt(0)
	v_max_f32_e32 v226, v226, v226
	v_max_f32_e32 v227, v227, v227
	v_max_f32_e32 v228, v228, v228
	v_max_f32_e32 v229, v229, v229
	v_max_f32_e32 v230, v230, v230
	v_max_f32_e32 v231, v231, v231
	v_max_f32_e32 v232, v232, v232
	v_max_f32_e32 v233, v233, v233
	v_max_f32_e32 v234, v234, v234
	v_max_f32_e32 v235, v235, v235
	v_max_f32_e32 v236, v236, v236
	v_max_f32_e32 v237, v237, v237
	v_max_f32_e32 v238, v238, v238
	v_max_f32_e32 v239, v239, v239
	v_max_f32_e32 v240, v240, v240
	v_max_f32_e32 v241, v241, v241
	v_med3_f32 v226, v226, s62, v95
	v_med3_f32 v227, v227, s62, v95
	v_med3_f32 v228, v228, s62, v95
	v_med3_f32 v229, v229, s62, v95
	v_med3_f32 v230, v230, s62, v95
	v_med3_f32 v231, v231, s62, v95
	v_med3_f32 v232, v232, s62, v95
	v_med3_f32 v233, v233, s62, v95
	v_med3_f32 v234, v234, s62, v95
	v_med3_f32 v235, v235, s62, v95
	v_med3_f32 v236, v236, s62, v95
	v_med3_f32 v237, v237, s62, v95
	v_med3_f32 v238, v238, s62, v95
	v_med3_f32 v239, v239, s62, v95
	v_med3_f32 v240, v240, s62, v95
	v_med3_f32 v241, v241, s62, v95
	v_mov_b32_e32 v242, 0
	v_mov_b32_e32 v243, 0
	v_mov_b32_e32 v244, 0
	v_mov_b32_e32 v245, 0
	v_cvt_pk_fp8_f32 v242, v226, v227
	v_cvt_pk_fp8_f32 v243, v230, v231
	v_cvt_pk_fp8_f32 v244, v234, v235
	v_cvt_pk_fp8_f32 v245, v238, v239
	v_cvt_pk_fp8_f32 v242, v228, v229 op_sel:[0,0,1]
	v_cvt_pk_fp8_f32 v243, v232, v233 op_sel:[0,0,1]
	v_cvt_pk_fp8_f32 v244, v236, v237 op_sel:[0,0,1]
	v_cvt_pk_fp8_f32 v245, v240, v241 op_sel:[0,0,1]
	s_nop 0
	global_store_dwordx4 v79, v[242:245], s[6:7]
	ds_read_b32 v226, v214
	ds_read_b32 v227, v214 offset:512
	ds_read_b32 v228, v214 offset:1024
	ds_read_b32 v229, v214 offset:1536
	ds_read_b32 v230, v214 offset:2048
	ds_read_b32 v231, v214 offset:2560
	ds_read_b32 v232, v214 offset:3072
	ds_read_b32 v233, v214 offset:3584
	ds_read_b32 v234, v214 offset:4096
	ds_read_b32 v235, v214 offset:4608
	ds_read_b32 v236, v214 offset:5120
	ds_read_b32 v237, v214 offset:5632
	ds_read_b32 v238, v214 offset:6144
	ds_read_b32 v239, v214 offset:6656
	ds_read_b32 v240, v214 offset:7168
	ds_read_b32 v241, v214 offset:7680
	s_waitcnt lgkmcnt(0)
; #define GAS __attribute__((address_space(1)))
; #define LAS __attribute__((address_space(3)))
; #define LDS_WAIT() asm volatile("s_waitcnt lgkmcnt(0)" ::: "memory")
; __device__ __forceinline__ int src_col_in(int c) {
;     if (c < 5120) { const int blk = c >> 7, p = c & 127; const bool rope = blk < 16 || ((((blk - 16) >> 2) & 1) == 0); const int d = rope ? (p >> 1) + 64 * (p & 1) : p; return blk * 128 + d; }
;     if (c < OFF_Z) return c + 2096;
;     if (c < OFF_G) return c - 4048;
;     if (c < OFF_DT) return 5120 + (c - OFF_G);
;     if (c < NSRC) return c;
;     return -1;
; }
;     const int pr = item >> 1, kb = 2 * (pr / nblk) + (item & 1), nb = pr % nblk, k0 = 64 * kb, n0 = 32 * nb;
;     const int nr = n0 + (lane & 31); const int sc = MAP == 1 ? src_col_in(nr) : nr;
;     float v[32];
; #pragma unroll
;     for (int i = 0; i < 32; ++i) v[i] = sc >= 0 ? W[(size_t)(k0 + 2 * i + (lane >> 5)) * Nsrc + sc] : 0.f;
; #pragma unroll
;     for (int i = 0; i < 32; ++i) { const int k = k0 + 2 * i + (lane >> 5); float x = v[i] * wscale; if (KS) x *= (k < ksplit ? ksA[k] : ksB[k - ksplit]); scr[(2 * i + (lane >> 5)) * 33 + (lane & 31)] = x; }
;     LDS_WAIT(); asm volatile("" ::: "memory");
;     const int c = lane & 7;
; #pragma unroll
;     for (int j = 0; j < 4; ++j) { const int n = (lane >> 3) + 8 * j; const LAS float* s = scr + (8 * c) * 33 + n;
;         const unsigned long long o = (unsigned long long)pg8::pk4_fp8(s[0 * 33], s[1 * 33], s[2 * 33], s[3 * 33]) | ((unsigned long long)pg8::pk4_fp8(s[4 * 33], s[5 * 33], s[6 * 33], s[7 * 33]) << 32);
;         *(GAS unsigned long long*)(WT + (size_t)(n0 + n) * K + k0 + 8 * c) = o; }
;     LDS_WAIT(); asm volatile("" ::: "memory");
; }
	v_max_f32_e32 v226, v226, v226
	v_max_f32_e32 v227, v227, v227
	v_max_f32_e32 v228, v228, v228
	v_max_f32_e32 v229, v229, v229
	v_max_f32_e32 v230, v230, v230
	v_max_f32_e32 v231, v231, v231
	v_max_f32_e32 v232, v232, v232
	v_max_f32_e32 v233, v233, v233
	v_max_f32_e32 v234, v234, v234
	v_max_f32_e32 v235, v235, v235
	v_max_f32_e32 v236, v236, v236
	v_max_f32_e32 v237, v237, v237
	v_max_f32_e32 v238, v238, v238
	v_max_f32_e32 v239, v239, v239
	v_max_f32_e32 v240, v240, v240
	v_max_f32_e32 v241, v241, v241
	v_med3_f32 v226, v226, s62, v95
	v_med3_f32 v227, v227, s62, v95
	v_med3_f32 v228, v228, s62, v95
	v_med3_f32 v229, v229, s62, v95
	v_med3_f32 v230, v230, s62, v95
	v_med3_f32 v231, v231, s62, v95
	v_med3_f32 v232, v232, s62, v95
	v_med3_f32 v233, v233, s62, v95
	v_med3_f32 v234, v234, s62, v95
	v_med3_f32 v235, v235, s62, v95
	v_med3_f32 v236, v236, s62, v95
	v_med3_f32 v237, v237, s62, v95
	v_med3_f32 v238, v238, s62, v95
	v_med3_f32 v239, v239, s62, v95
	v_med3_f32 v240, v240, s62, v95
	v_med3_f32 v241, v241, s62, v95
	v_mov_b32_e32 v242, 0
	v_mov_b32_e32 v243, 0
	v_mov_b32_e32 v244, 0
	v_mov_b32_e32 v245, 0
	v_cvt_pk_fp8_f32 v242, v226, v227
	v_cvt_pk_fp8_f32 v243, v230, v231
	v_cvt_pk_fp8_f32 v244, v234, v235
	v_cvt_pk_fp8_f32 v245, v238, v239
	v_cvt_pk_fp8_f32 v242, v228, v229 op_sel:[0,0,1]
	v_cvt_pk_fp8_f32 v243, v232, v233 op_sel:[0,0,1]
	v_cvt_pk_fp8_f32 v244, v236, v237 op_sel:[0,0,1]
	v_cvt_pk_fp8_f32 v245, v240, v241 op_sel:[0,0,1]
	s_nop 0
	global_store_dwordx4 v80, v[242:245], s[6:7]
	s_waitcnt vmcnt(12)
	v_mul_f32_e32 v144, 0x43000000, v144
	v_mul_f32_e32 v145, 0x43000000, v145
	v_mul_f32_e32 v146, 0x43000000, v146
	v_mul_f32_e32 v147, 0x43000000, v147
	ds_write_b128 v209, v[144:147]
	v_mul_f32_e32 v148, 0x43000000, v148
	v_mul_f32_e32 v149, 0x43000000, v149
	v_mul_f32_e32 v150, 0x43000000, v150
	v_mul_f32_e32 v151, 0x43000000, v151
	ds_write_b128 v209, v[148:151] offset:1024
	v_mul_f32_e32 v152, 0x43000000, v152
	v_mul_f32_e32 v153, 0x43000000, v153
	v_mul_f32_e32 v154, 0x43000000, v154
	v_mul_f32_e32 v155, 0x43000000, v155
	ds_write_b128 v209, v[152:155] offset:2048
	v_mul_f32_e32 v156, 0x43000000, v156
	v_mul_f32_e32 v157, 0x43000000, v157
	v_mul_f32_e32 v158, 0x43000000, v158
	v_mul_f32_e32 v159, 0x43000000, v159
	ds_write_b128 v209, v[156:159] offset:3072
	v_mul_f32_e32 v160, 0x43000000, v160
	v_mul_f32_e32 v161, 0x43000000, v161
	v_mul_f32_e32 v162, 0x43000000, v162
	v_mul_f32_e32 v163, 0x43000000, v163
	ds_write_b128 v209, v[160:163] offset:4096
	v_mul_f32_e32 v164, 0x43000000, v164
	v_mul_f32_e32 v165, 0x43000000, v165
	v_mul_f32_e32 v166, 0x43000000, v166
	v_mul_f32_e32 v167, 0x43000000, v167
	ds_write_b128 v209, v[164:167] offset:5120
	v_mul_f32_e32 v168, 0x43000000, v168
	v_mul_f32_e32 v169, 0x43000000, v169
	v_mul_f32_e32 v170, 0x43000000, v170
	v_mul_f32_e32 v171, 0x43000000, v171
	ds_write_b128 v209, v[168:171] offset:6144
	v_mul_f32_e32 v172, 0x43000000, v172
	v_mul_f32_e32 v173, 0x43000000, v173
	v_mul_f32_e32 v174, 0x43000000, v174
	v_mul_f32_e32 v175, 0x43000000, v175
	ds_write_b128 v209, v[172:175] offset:7168
	s_waitcnt lgkmcnt(0)
	s_barrier
	s_add_i32 s24, s23, 0
	s_lshl_b32 s20, s24, 7
	s_cmp_lt_u32 s24, 40
	s_cselect_b32 s21, 0, 0x830
	s_cmp_lt_u32 s24, 72
	s_cselect_b32 s21, s21, 0xfffff030
	s_add_i32 s20, s20, s21
	s_lshl_b32 s20, s20, 2
	s_add_u32 s8, s46, s20
	s_addc_u32 s9, s47, 0
	global_load_dwordx4 v[144:147], v76, s[8:9]
	s_add_u32 s8, s8, 0x16280
	s_addc_u32 s9, s9, 0
	global_load_dwordx4 v[148:151], v76, s[8:9]
	s_add_u32 s8, s8, 0x16280
	s_addc_u32 s9, s9, 0
	global_load_dwordx4 v[152:155], v76, s[8:9]
	s_add_u32 s8, s8, 0x16280
	s_addc_u32 s9, s9, 0
	global_load_dwordx4 v[156:159], v76, s[8:9]
	s_add_u32 s8, s8, 0x16280
	s_addc_u32 s9, s9, 0
	global_load_dwordx4 v[160:163], v76, s[8:9]
	s_add_u32 s8, s8, 0x16280
	s_addc_u32 s9, s9, 0
	global_load_dwordx4 v[164:167], v76, s[8:9]
	s_add_u32 s8, s8, 0x16280
	s_addc_u32 s9, s9, 0
	global_load_dwordx4 v[168:171], v76, s[8:9]
	s_add_u32 s8, s8, 0x16280
	s_addc_u32 s9, s9, 0
	global_load_dwordx4 v[172:175], v76, s[8:9]
	s_add_u32 s6, s40, 0x2003000
	s_addc_u32 s7, s41, 0
	ds_read_b32 v226, v211
	ds_read_b32 v227, v211 offset:512
	ds_read_b32 v228, v211 offset:1024
	ds_read_b32 v229, v211 offset:1536
	ds_read_b32 v230, v211 offset:2048
	ds_read_b32 v231, v211 offset:2560
	ds_read_b32 v232, v211 offset:3072
	ds_read_b32 v233, v211 offset:3584
	ds_read_b32 v234, v211 offset:4096
	ds_read_b32 v235, v211 offset:4608
	ds_read_b32 v236, v211 offset:5120
	ds_read_b32 v237, v211 offset:5632
	ds_read_b32 v238, v211 offset:6144
	ds_read_b32 v239, v211 offset:6656
	ds_read_b32 v240, v211 offset:7168
	ds_read_b32 v241, v211 offset:7680
	s_waitcnt lgkmcnt(0)
; #define GAS __attribute__((address_space(1)))
; #define LAS __attribute__((address_space(3)))
; #define LDS_WAIT() asm volatile("s_waitcnt lgkmcnt(0)" ::: "memory")
;     const int pr = item >> 1, kb = 2 * (pr / nblk) + (item & 1), nb = pr % nblk, k0 = 64 * kb, n0 = 32 * nb;
;     const int nr = n0 + (lane & 31); const int sc = MAP == 1 ? src_col_in(nr) : nr;
;     float v[32];
; #pragma unroll
;     for (int i = 0; i < 32; ++i) v[i] = sc >= 0 ? W[(size_t)(k0 + 2 * i + (lane >> 5)) * Nsrc + sc] : 0.f;
; #pragma unroll
;     for (int i = 0; i < 32; ++i) { const int k = k0 + 2 * i + (lane >> 5); float x = v[i] * wscale; if (KS) x *= (k < ksplit ? ksA[k] : ksB[k - ksplit]); scr[(2 * i + (lane >> 5)) * 33 + (lane & 31)] = x; }
;     LDS_WAIT(); asm volatile("" ::: "memory");
;     const int c = lane & 7;
; #pragma unroll
;     for (int j = 0; j < 4; ++j) { const int n = (lane >> 3) + 8 * j; const LAS float* s = scr + (8 * c) * 33 + n;
;         const unsigned long long o = (unsigned long long)pg8::pk4_fp8(s[0 * 33], s[1 * 33], s[2 * 33], s[3 * 33]) | ((unsigned long long)pg8::pk4_fp8(s[4 * 33], s[5 * 33], s[6 * 33], s[7 * 33]) << 32);
;         *(GAS unsigned long long*)(WT + (size_t)(n0 + n) * K + k0 + 8 * c) = o; }
;     LDS_WAIT(); asm volatile("" ::: "memory");
	v_max_f32_e32 v226, v226, v226
	v_max_f32_e32 v227, v227, v227
	v_max_f32_e32 v228, v228, v228
	v_max_f32_e32 v229, v229, v229
	v_max_f32_e32 v230, v230, v230
	v_max_f32_e32 v231, v231, v231
	v_max_f32_e32 v232, v232, v232
	v_max_f32_e32 v233, v233, v233
	v_max_f32_e32 v234, v234, v234
	v_max_f32_e32 v235, v235, v235
	v_max_f32_e32 v236, v236, v236
	v_max_f32_e32 v237, v237, v237
	v_max_f32_e32 v238, v238, v238
	v_max_f32_e32 v239, v239, v239
	v_max_f32_e32 v240, v240, v240
	v_max_f32_e32 v241, v241, v241
	v_med3_f32 v226, v226, s62, v95
	v_med3_f32 v227, v227, s62, v95
	v_med3_f32 v228, v228, s62, v95
	v_med3_f32 v229, v229, s62, v95
	v_med3_f32 v230, v230, s62, v95
	v_med3_f32 v231, v231, s62, v95
	v_med3_f32 v232, v232, s62, v95
	v_med3_f32 v233, v233, s62, v95
	v_med3_f32 v234, v234, s62, v95
	v_med3_f32 v235, v235, s62, v95
	v_med3_f32 v236, v236, s62, v95
	v_med3_f32 v237, v237, s62, v95
	v_med3_f32 v238, v238, s62, v95
	v_med3_f32 v239, v239, s62, v95
	v_med3_f32 v240, v240, s62, v95
	v_med3_f32 v241, v241, s62, v95
	v_mov_b32_e32 v242, 0
	v_mov_b32_e32 v243, 0
	v_mov_b32_e32 v244, 0
	v_mov_b32_e32 v245, 0
	v_cvt_pk_fp8_f32 v242, v226, v227
	v_cvt_pk_fp8_f32 v243, v230, v231
	v_cvt_pk_fp8_f32 v244, v234, v235
	v_cvt_pk_fp8_f32 v245, v238, v239
	v_cvt_pk_fp8_f32 v242, v228, v229 op_sel:[0,0,1]
	v_cvt_pk_fp8_f32 v243, v232, v233 op_sel:[0,0,1]
	v_cvt_pk_fp8_f32 v244, v236, v237 op_sel:[0,0,1]
	v_cvt_pk_fp8_f32 v245, v240, v241 op_sel:[0,0,1]
	s_nop 0
	global_store_dwordx4 v79, v[242:245], s[6:7]
	ds_read_b32 v226, v213
	ds_read_b32 v227, v213 offset:512
	ds_read_b32 v228, v213 offset:1024
	ds_read_b32 v229, v213 offset:1536
	ds_read_b32 v230, v213 offset:2048
	ds_read_b32 v231, v213 offset:2560
	ds_read_b32 v232, v213 offset:3072
	ds_read_b32 v233, v213 offset:3584
	ds_read_b32 v234, v213 offset:4096
	ds_read_b32 v235, v213 offset:4608
	ds_read_b32 v236, v213 offset:5120
	ds_read_b32 v237, v213 offset:5632
	ds_read_b32 v238, v213 offset:6144
	ds_read_b32 v239, v213 offset:6656
	ds_read_b32 v240, v213 offset:7168
	ds_read_b32 v241, v213 offset:7680
	s_waitcnt lgkmcnt(0)
	v_max_f32_e32 v226, v226, v226
	v_max_f32_e32 v227, v227, v227
	v_max_f32_e32 v228, v228, v228
	v_max_f32_e32 v229, v229, v229
	v_max_f32_e32 v230, v230, v230
	v_max_f32_e32 v231, v231, v231
	v_max_f32_e32 v232, v232, v232
	v_max_f32_e32 v233, v233, v233
	v_max_f32_e32 v234, v234, v234
	v_max_f32_e32 v235, v235, v235
	v_max_f32_e32 v236, v236, v236
	v_max_f32_e32 v237, v237, v237
	v_max_f32_e32 v238, v238, v238
	v_max_f32_e32 v239, v239, v239
	v_max_f32_e32 v240, v240, v240
	v_max_f32_e32 v241, v241, v241
	v_med3_f32 v226, v226, s62, v95
	v_med3_f32 v227, v227, s62, v95
	v_med3_f32 v228, v228, s62, v95
	v_med3_f32 v229, v229, s62, v95
	v_med3_f32 v230, v230, s62, v95
	v_med3_f32 v231, v231, s62, v95
	v_med3_f32 v232, v232, s62, v95
	v_med3_f32 v233, v233, s62, v95
	v_med3_f32 v234, v234, s62, v95
	v_med3_f32 v235, v235, s62, v95
	v_med3_f32 v236, v236, s62, v95
	v_med3_f32 v237, v237, s62, v95
	v_med3_f32 v238, v238, s62, v95
	v_med3_f32 v239, v239, s62, v95
	v_med3_f32 v240, v240, s62, v95
	v_med3_f32 v241, v241, s62, v95
	v_mov_b32_e32 v242, 0
	v_mov_b32_e32 v243, 0
	v_mov_b32_e32 v244, 0
	v_mov_b32_e32 v245, 0
	v_cvt_pk_fp8_f32 v242, v226, v227
	v_cvt_pk_fp8_f32 v243, v230, v231
	v_cvt_pk_fp8_f32 v244, v234, v235
	v_cvt_pk_fp8_f32 v245, v238, v239
	v_cvt_pk_fp8_f32 v242, v228, v229 op_sel:[0,0,1]
	v_cvt_pk_fp8_f32 v243, v232, v233 op_sel:[0,0,1]
	v_cvt_pk_fp8_f32 v244, v236, v237 op_sel:[0,0,1]
	v_cvt_pk_fp8_f32 v245, v240, v241 op_sel:[0,0,1]
	s_nop 0
	global_store_dwordx4 v80, v[242:245], s[6:7]
	s_waitcnt vmcnt(12)
	v_mul_f32_e32 v176, 0x43000000, v176
	v_mul_f32_e32 v177, 0x43000000, v177
	v_mul_f32_e32 v178, 0x43000000, v178
	v_mul_f32_e32 v179, 0x43000000, v179
	ds_write_b128 v210, v[176:179]
	v_mul_f32_e32 v180, 0x43000000, v180
	v_mul_f32_e32 v181, 0x43000000, v181
	v_mul_f32_e32 v182, 0x43000000, v182
	v_mul_f32_e32 v183, 0x43000000, v183
	ds_write_b128 v210, v[180:183] offset:1024
	v_mul_f32_e32 v184, 0x43000000, v184
	v_mul_f32_e32 v185, 0x43000000, v185
	v_mul_f32_e32 v186, 0x43000000, v186
	v_mul_f32_e32 v187, 0x43000000, v187
	ds_write_b128 v210, v[184:187] offset:2048
	v_mul_f32_e32 v188, 0x43000000, v188
	v_mul_f32_e32 v189, 0x43000000, v189
	v_mul_f32_e32 v190, 0x43000000, v190
	v_mul_f32_e32 v191, 0x43000000, v191
	ds_write_b128 v210, v[188:191] offset:3072
	v_mul_f32_e32 v192, 0x43000000, v192
	v_mul_f32_e32 v193, 0x43000000, v193
	v_mul_f32_e32 v194, 0x43000000, v194
	v_mul_f32_e32 v195, 0x43000000, v195
	ds_write_b128 v210, v[192:195] offset:4096
	v_mul_f32_e32 v196, 0x43000000, v196
	v_mul_f32_e32 v197, 0x43000000, v197
	v_mul_f32_e32 v198, 0x43000000, v198
	v_mul_f32_e32 v199, 0x43000000, v199
	ds_write_b128 v210, v[196:199] offset:5120
	v_mul_f32_e32 v200, 0x43000000, v200
	v_mul_f32_e32 v201, 0x43000000, v201
	v_mul_f32_e32 v202, 0x43000000, v202
	v_mul_f32_e32 v203, 0x43000000, v203
	ds_write_b128 v210, v[200:203] offset:6144
	v_mul_f32_e32 v204, 0x43000000, v204
	v_mul_f32_e32 v205, 0x43000000, v205
	v_mul_f32_e32 v206, 0x43000000, v206
	v_mul_f32_e32 v207, 0x43000000, v207
	ds_write_b128 v210, v[204:207] offset:7168
	s_waitcnt lgkmcnt(0)
	s_barrier
; #define GAS __attribute__((address_space(1)))
; #define LAS __attribute__((address_space(3)))
; #define LDS_WAIT() asm volatile("s_waitcnt lgkmcnt(0)" ::: "memory")
; __device__ __forceinline__ int src_col_in(int c) {
;     if (c < 5120) { const int blk = c >> 7, p = c & 127; const bool rope = blk < 16 || ((((blk - 16) >> 2) & 1) == 0); const int d = rope ? (p >> 1) + 64 * (p & 1) : p; return blk * 128 + d; }
;     if (c < OFF_Z) return c + 2096;
;     if (c < OFF_G) return c - 4048;
;     if (c < OFF_DT) return 5120 + (c - OFF_G);
;     if (c < NSRC) return c;
;     return -1;
;     const int pr = item >> 1, kb = 2 * (pr / nblk) + (item & 1), nb = pr % nblk, k0 = 64 * kb, n0 = 32 * nb;
;     const int nr = n0 + (lane & 31); const int sc = MAP == 1 ? src_col_in(nr) : nr;
;     float v[32];
; #pragma unroll
;     for (int i = 0; i < 32; ++i) v[i] = sc >= 0 ? W[(size_t)(k0 + 2 * i + (lane >> 5)) * Nsrc + sc] : 0.f;
; #pragma unroll
;     for (int i = 0; i < 32; ++i) { const int k = k0 + 2 * i + (lane >> 5); float x = v[i] * wscale; if (KS) x *= (k < ksplit ? ksA[k] : ksB[k - ksplit]); scr[(2 * i + (lane >> 5)) * 33 + (lane & 31)] = x; }
;     LDS_WAIT(); asm volatile("" ::: "memory");
;     const int c = lane & 7;
; #pragma unroll
;     for (int j = 0; j < 4; ++j) { const int n = (lane >> 3) + 8 * j; const LAS float* s = scr + (8 * c) * 33 + n;
;         const unsigned long long o = (unsigned long long)pg8::pk4_fp8(s[0 * 33], s[1 * 33], s[2 * 33], s[3 * 33]) | ((unsigned long long)pg8::pk4_fp8(s[4 * 33], s[5 * 33], s[6 * 33], s[7 * 33]) << 32);
;         *(GAS unsigned long long*)(WT + (size_t)(n0 + n) * K + k0 + 8 * c) = o; }
;     LDS_WAIT(); asm volatile("" ::: "memory");
	s_add_i32 s24, s23, 8
	s_lshl_b32 s20, s24, 7
	s_cmp_lt_u32 s24, 40
	s_cselect_b32 s21, 0, 0x830
	s_cmp_lt_u32 s24, 72
	s_cselect_b32 s21, s21, 0xfffff030
	s_add_i32 s20, s20, s21
	s_lshl_b32 s20, s20, 2
	s_add_u32 s8, s46, s20
	s_addc_u32 s9, s47, 0
	global_load_dwordx4 v[176:179], v76, s[8:9]
	s_add_u32 s8, s8, 0x16280
	s_addc_u32 s9, s9, 0
	global_load_dwordx4 v[180:183], v76, s[8:9]
	s_add_u32 s8, s8, 0x16280
	s_addc_u32 s9, s9, 0
	global_load_dwordx4 v[184:187], v76, s[8:9]
	s_add_u32 s8, s8, 0x16280
	s_addc_u32 s9, s9, 0
	global_load_dwordx4 v[188:191], v76, s[8:9]
	s_add_u32 s8, s8, 0x16280
	s_addc_u32 s9, s9, 0
	global_load_dwordx4 v[192:195], v76, s[8:9]
	s_add_u32 s8, s8, 0x16280
	s_addc_u32 s9, s9, 0
	global_load_dwordx4 v[196:199], v76, s[8:9]
	s_add_u32 s8, s8, 0x16280
	s_addc_u32 s9, s9, 0
	global_load_dwordx4 v[200:203], v76, s[8:9]
	s_add_u32 s8, s8, 0x16280
	s_addc_u32 s9, s9, 0
	global_load_dwordx4 v[204:207], v76, s[8:9]
	s_add_u32 s6, s40, 0x3003000
	s_addc_u32 s7, s41, 0
	ds_read_b32 v226, v212
	ds_read_b32 v227, v212 offset:512
	ds_read_b32 v228, v212 offset:1024
	ds_read_b32 v229, v212 offset:1536
	ds_read_b32 v230, v212 offset:2048
	ds_read_b32 v231, v212 offset:2560
	ds_read_b32 v232, v212 offset:3072
	ds_read_b32 v233, v212 offset:3584
	ds_read_b32 v234, v212 offset:4096
	ds_read_b32 v235, v212 offset:4608
	ds_read_b32 v236, v212 offset:5120
	ds_read_b32 v237, v212 offset:5632
	ds_read_b32 v238, v212 offset:6144
	ds_read_b32 v239, v212 offset:6656
	ds_read_b32 v240, v212 offset:7168
	ds_read_b32 v241, v212 offset:7680
	s_waitcnt lgkmcnt(0)
	v_max_f32_e32 v226, v226, v226
	v_max_f32_e32 v227, v227, v227
	v_max_f32_e32 v228, v228, v228
	v_max_f32_e32 v229, v229, v229
	v_max_f32_e32 v230, v230, v230
	v_max_f32_e32 v231, v231, v231
	v_max_f32_e32 v232, v232, v232
	v_max_f32_e32 v233, v233, v233
	v_max_f32_e32 v234, v234, v234
	v_max_f32_e32 v235, v235, v235
	v_max_f32_e32 v236, v236, v236
	v_max_f32_e32 v237, v237, v237
	v_max_f32_e32 v238, v238, v238
	v_max_f32_e32 v239, v239, v239
	v_max_f32_e32 v240, v240, v240
	v_max_f32_e32 v241, v241, v241
	v_med3_f32 v226, v226, s62, v95
	v_med3_f32 v227, v227, s62, v95
	v_med3_f32 v228, v228, s62, v95
	v_med3_f32 v229, v229, s62, v95
	v_med3_f32 v230, v230, s62, v95
	v_med3_f32 v231, v231, s62, v95
	v_med3_f32 v232, v232, s62, v95
	v_med3_f32 v233, v233, s62, v95
	v_med3_f32 v234, v234, s62, v95
	v_med3_f32 v235, v235, s62, v95
	v_med3_f32 v236, v236, s62, v95
	v_med3_f32 v237, v237, s62, v95
	v_med3_f32 v238, v238, s62, v95
	v_med3_f32 v239, v239, s62, v95
	v_med3_f32 v240, v240, s62, v95
	v_med3_f32 v241, v241, s62, v95
	v_mov_b32_e32 v242, 0
	v_mov_b32_e32 v243, 0
	v_mov_b32_e32 v244, 0
	v_mov_b32_e32 v245, 0
	v_cvt_pk_fp8_f32 v242, v226, v227
	v_cvt_pk_fp8_f32 v243, v230, v231
	v_cvt_pk_fp8_f32 v244, v234, v235
	v_cvt_pk_fp8_f32 v245, v238, v239
	v_cvt_pk_fp8_f32 v242, v228, v229 op_sel:[0,0,1]
	v_cvt_pk_fp8_f32 v243, v232, v233 op_sel:[0,0,1]
	v_cvt_pk_fp8_f32 v244, v236, v237 op_sel:[0,0,1]
	v_cvt_pk_fp8_f32 v245, v240, v241 op_sel:[0,0,1]
	s_nop 0
	global_store_dwordx4 v79, v[242:245], s[6:7]
	ds_read_b32 v226, v214
	ds_read_b32 v227, v214 offset:512
	ds_read_b32 v228, v214 offset:1024
	ds_read_b32 v229, v214 offset:1536
	ds_read_b32 v230, v214 offset:2048
	ds_read_b32 v231, v214 offset:2560
	ds_read_b32 v232, v214 offset:3072
	ds_read_b32 v233, v214 offset:3584
	ds_read_b32 v234, v214 offset:4096
	ds_read_b32 v235, v214 offset:4608
	ds_read_b32 v236, v214 offset:5120
	ds_read_b32 v237, v214 offset:5632
	ds_read_b32 v238, v214 offset:6144
	ds_read_b32 v239, v214 offset:6656
	ds_read_b32 v240, v214 offset:7168
	ds_read_b32 v241, v214 offset:7680
	s_waitcnt lgkmcnt(0)
	v_max_f32_e32 v226, v226, v226
	v_max_f32_e32 v227, v227, v227
	v_max_f32_e32 v228, v228, v228
	v_max_f32_e32 v229, v229, v229
	v_max_f32_e32 v230, v230, v230
	v_max_f32_e32 v231, v231, v231
	v_max_f32_e32 v232, v232, v232
	v_max_f32_e32 v233, v233, v233
	v_max_f32_e32 v234, v234, v234
	v_max_f32_e32 v235, v235, v235
	v_max_f32_e32 v236, v236, v236
	v_max_f32_e32 v237, v237, v237
	v_max_f32_e32 v238, v238, v238
	v_max_f32_e32 v239, v239, v239
	v_max_f32_e32 v240, v240, v240
	v_max_f32_e32 v241, v241, v241
	v_med3_f32 v226, v226, s62, v95
	v_med3_f32 v227, v227, s62, v95
	v_med3_f32 v228, v228, s62, v95
	v_med3_f32 v229, v229, s62, v95
	v_med3_f32 v230, v230, s62, v95
	v_med3_f32 v231, v231, s62, v95
	v_med3_f32 v232, v232, s62, v95
	v_med3_f32 v233, v233, s62, v95
	v_med3_f32 v234, v234, s62, v95
	v_med3_f32 v235, v235, s62, v95
	v_med3_f32 v236, v236, s62, v95
	v_med3_f32 v237, v237, s62, v95
	v_med3_f32 v238, v238, s62, v95
	v_med3_f32 v239, v239, s62, v95
	v_med3_f32 v240, v240, s62, v95
	v_med3_f32 v241, v241, s62, v95
	v_mov_b32_e32 v242, 0
	v_mov_b32_e32 v243, 0
	v_mov_b32_e32 v244, 0
	v_mov_b32_e32 v245, 0
	v_cvt_pk_fp8_f32 v242, v226, v227
	v_cvt_pk_fp8_f32 v243, v230, v231
	v_cvt_pk_fp8_f32 v244, v234, v235
	v_cvt_pk_fp8_f32 v245, v238, v239
	v_cvt_pk_fp8_f32 v242, v228, v229 op_sel:[0,0,1]
	v_cvt_pk_fp8_f32 v243, v232, v233 op_sel:[0,0,1]
	v_cvt_pk_fp8_f32 v244, v236, v237 op_sel:[0,0,1]
	v_cvt_pk_fp8_f32 v245, v240, v241 op_sel:[0,0,1]
	s_nop 0
	global_store_dwordx4 v80, v[242:245], s[6:7]
	s_waitcnt vmcnt(12)
	v_mul_f32_e32 v144, v42, v144
	v_mul_f32_e32 v145, v42, v145
	v_mul_f32_e32 v146, v42, v146
	v_mul_f32_e32 v147, v42, v147
	ds_write_b128 v209, v[144:147]
	v_mul_f32_e32 v148, v43, v148
	v_mul_f32_e32 v149, v43, v149
	v_mul_f32_e32 v150, v43, v150
	v_mul_f32_e32 v151, v43, v151
	ds_write_b128 v209, v[148:151] offset:1024
	v_mul_f32_e32 v152, v44, v152
	v_mul_f32_e32 v153, v44, v153
	v_mul_f32_e32 v154, v44, v154
	v_mul_f32_e32 v155, v44, v155
	ds_write_b128 v209, v[152:155] offset:2048
	v_mul_f32_e32 v156, v45, v156
	v_mul_f32_e32 v157, v45, v157
	v_mul_f32_e32 v158, v45, v158
	v_mul_f32_e32 v159, v45, v159
	ds_write_b128 v209, v[156:159] offset:3072
	v_mul_f32_e32 v160, v46, v160
	v_mul_f32_e32 v161, v46, v161
	v_mul_f32_e32 v162, v46, v162
	v_mul_f32_e32 v163, v46, v163
	ds_write_b128 v209, v[160:163] offset:4096
	v_mul_f32_e32 v164, v47, v164
	v_mul_f32_e32 v165, v47, v165
	v_mul_f32_e32 v166, v47, v166
	v_mul_f32_e32 v167, v47, v167
	ds_write_b128 v209, v[164:167] offset:5120
	v_mul_f32_e32 v168, v48, v168
	v_mul_f32_e32 v169, v48, v169
	v_mul_f32_e32 v170, v48, v170
	v_mul_f32_e32 v171, v48, v171
	ds_write_b128 v209, v[168:171] offset:6144
	v_mul_f32_e32 v172, v49, v172
	v_mul_f32_e32 v173, v49, v173
	v_mul_f32_e32 v174, v49, v174
	v_mul_f32_e32 v175, v49, v175
	ds_write_b128 v209, v[172:175] offset:7168
	s_waitcnt lgkmcnt(0)
	s_barrier
; #define GAS __attribute__((address_space(1)))
; #define LAS __attribute__((address_space(3)))
; #define LDS_WAIT() asm volatile("s_waitcnt lgkmcnt(0)" ::: "memory")
; __device__ __forceinline__ unsigned pk2(float lo, float hi) { return f2bf(lo) | (f2bf(hi) << 16); }
; __device__ __forceinline__ int nat_dim(int p) { return (p >> 1) + 64 * (p & 1); }
; __device__ __forceinline__ int src_col_in(int c) {
;     if (c < 5120) { const int blk = c >> 7, p = c & 127; const bool rope = blk < 16 || ((((blk - 16) >> 2) & 1) == 0); const int d = rope ? (p >> 1) + 64 * (p & 1) : p; return blk * 128 + d; }
;     if (c < OFF_Z) return c + 2096;
;     if (c < OFF_G) return c - 4048;
;     if (c < OFF_DT) return 5120 + (c - OFF_G);
;     if (c < NSRC) return c;
;     return -1;
; template <int MAP, bool KS, bool KPERM = false>
; __device__ __forceinline__ void p0_transpose_item(const float* W, int K, int Nsrc, int nblk, bf16* WT, const float* ksA, const float* ksB, int ksplit, LAS float* scr, int item, int lane) {
;     const int kb = item / nblk, nb = item % nblk, k0 = 64 * kb, n0 = 32 * nb;
;     const int nr = n0 + (lane & 31); const int sc = MAP == 1 ? src_col_in(nr) : (MAP == 2 ? nat_dim(nr) : nr);
;     float v[32];
; #pragma unroll
;     for (int i = 0; i < 32; ++i) { const int k = k0 + 2 * i + (lane >> 5); const int ksrc = KPERM ? ((k & ~127) + nat_dim(k & 127)) : k;
;         v[i] = sc >= 0 ? W[(size_t)ksrc * Nsrc + sc] : 0.f; }
; #pragma unroll
;     for (int i = 0; i < 32; ++i) { const int kk = 2 * i + (lane >> 5); const int k = k0 + kk;
;         if (KS) v[i] *= (k < ksplit ? ksA[k] : ksB[k - ksplit]);
;         scr[kk * 33 + (lane & 31)] = v[i]; }
;     LDS_WAIT(); asm volatile("" ::: "memory");
;     const int c = lane & 7;
; #pragma unroll
;     for (int j = 0; j < 4; ++j) { const int n = (lane >> 3) + 8 * j; const LAS float* s = scr + (8 * c) * 33 + n;
;         v4u o; o.x = pk2(s[0 * 33], s[1 * 33]); o.y = pk2(s[2 * 33], s[3 * 33]); o.z = pk2(s[4 * 33], s[5 * 33]); o.w = pk2(s[6 * 33], s[7 * 33]);
;         *(GAS v4u*)(WT + (size_t)(n0 + n) * K + k0 + 8 * c) = o; }
;     LDS_WAIT(); asm volatile("" ::: "memory");
	s_add_i32 s24, s23, 16
	s_lshl_b32 s20, s24, 7
	s_cmp_lt_u32 s24, 40
	s_cselect_b32 s21, 0, 0x830
	s_cmp_lt_u32 s24, 72
	s_cselect_b32 s21, s21, 0xfffff030
	s_add_i32 s20, s20, s21
	s_lshl_b32 s20, s20, 2
	s_add_u32 s8, s46, s20
	s_addc_u32 s9, s47, 0
	global_load_dwordx4 v[144:147], v76, s[8:9]
	s_add_u32 s8, s8, 0x16280
	s_addc_u32 s9, s9, 0
	global_load_dwordx4 v[148:151], v76, s[8:9]
	s_add_u32 s8, s8, 0x16280
	s_addc_u32 s9, s9, 0
	global_load_dwordx4 v[152:155], v76, s[8:9]
	s_add_u32 s8, s8, 0x16280
	s_addc_u32 s9, s9, 0
	global_load_dwordx4 v[156:159], v76, s[8:9]
	s_add_u32 s8, s8, 0x16280
	s_addc_u32 s9, s9, 0
	global_load_dwordx4 v[160:163], v76, s[8:9]
	s_add_u32 s8, s8, 0x16280
	s_addc_u32 s9, s9, 0
	global_load_dwordx4 v[164:167], v76, s[8:9]
	s_add_u32 s8, s8, 0x16280
	s_addc_u32 s9, s9, 0
	global_load_dwordx4 v[168:171], v76, s[8:9]
	s_add_u32 s8, s8, 0x16280
	s_addc_u32 s9, s9, 0
	global_load_dwordx4 v[172:175], v76, s[8:9]
	s_add_i32 s24, s23, 0
	s_mul_i32 s20, s24, 0x100000
	s_add_u32 s6, s48, s20
	s_addc_u32 s7, s49, 0
	s_cmp_lt_u32 s24, 16
	s_cselect_b32 s20, 1, 0
	s_sub_i32 s21, s24, 16
	s_bitcmp0_b32 s21, 2
	s_cselect_b32 s21, 1, 0
	s_cmp_lt_u32 s24, 40
	s_cselect_b32 s21, s21, 0
	s_or_b32 s20, s20, s21
	s_cmp_lg_u32 s20, 0
	s_cselect_b64 s[20:21], -1, 0
	v_cndmask_b32_e64 v91, v83, v87, s[20:21]
	v_cndmask_b32_e64 v92, v84, v88, s[20:21]
	v_cndmask_b32_e64 v93, v85, v89, s[20:21]
	v_cndmask_b32_e64 v94, v86, v90, s[20:21]
	ds_read_b32 v226, v112
	ds_read_b32 v227, v112 offset:512
	ds_read_b32 v228, v112 offset:1024
	ds_read_b32 v229, v112 offset:1536
	ds_read_b32 v230, v112 offset:2048
	ds_read_b32 v231, v112 offset:2560
	ds_read_b32 v232, v112 offset:3072
	ds_read_b32 v233, v112 offset:3584
	s_waitcnt lgkmcnt(0)
	v_bfe_u32 v120, v226, 16, 1
	v_bfe_u32 v121, v227, 16, 1
	v_bfe_u32 v122, v228, 16, 1
	v_bfe_u32 v123, v229, 16, 1
	v_bfe_u32 v124, v230, 16, 1
	v_bfe_u32 v125, v231, 16, 1
	v_bfe_u32 v126, v232, 16, 1
	v_bfe_u32 v127, v233, 16, 1
	v_add3_u32 v226, v226, v120, s63
	v_add3_u32 v227, v227, v121, s63
	v_add3_u32 v228, v228, v122, s63
	v_add3_u32 v229, v229, v123, s63
	v_add3_u32 v230, v230, v124, s63
	v_add3_u32 v231, v231, v125, s63
	v_add3_u32 v232, v232, v126, s63
	v_add3_u32 v233, v233, v127, s63
	v_perm_b32 v242, v227, v226, s64
	v_perm_b32 v243, v229, v228, s64
	v_perm_b32 v244, v231, v230, s64
	v_perm_b32 v245, v233, v232, s64
	s_nop 0
	global_store_dwordx4 v91, v[242:245], s[6:7]
	ds_read_b32 v226, v114
	ds_read_b32 v227, v114 offset:512
	ds_read_b32 v228, v114 offset:1024
	ds_read_b32 v229, v114 offset:1536
	ds_read_b32 v230, v114 offset:2048
	ds_read_b32 v231, v114 offset:2560
	ds_read_b32 v232, v114 offset:3072
	ds_read_b32 v233, v114 offset:3584
	s_waitcnt lgkmcnt(0)
	v_bfe_u32 v120, v226, 16, 1
	v_bfe_u32 v121, v227, 16, 1
	v_bfe_u32 v122, v228, 16, 1
	v_bfe_u32 v123, v229, 16, 1
	v_bfe_u32 v124, v230, 16, 1
	v_bfe_u32 v125, v231, 16, 1
	v_bfe_u32 v126, v232, 16, 1
	v_bfe_u32 v127, v233, 16, 1
	v_add3_u32 v226, v226, v120, s63
	v_add3_u32 v227, v227, v121, s63
	v_add3_u32 v228, v228, v122, s63
	v_add3_u32 v229, v229, v123, s63
	v_add3_u32 v230, v230, v124, s63
	v_add3_u32 v231, v231, v125, s63
	v_add3_u32 v232, v232, v126, s63
	v_add3_u32 v233, v233, v127, s63
	v_perm_b32 v242, v227, v226, s64
	v_perm_b32 v243, v229, v228, s64
	v_perm_b32 v244, v231, v230, s64
	v_perm_b32 v245, v233, v232, s64
	s_nop 0
	global_store_dwordx4 v92, v[242:245], s[6:7]
	ds_read_b32 v226, v116
	ds_read_b32 v227, v116 offset:512
	ds_read_b32 v228, v116 offset:1024
	ds_read_b32 v229, v116 offset:1536
	ds_read_b32 v230, v116 offset:2048
	ds_read_b32 v231, v116 offset:2560
	ds_read_b32 v232, v116 offset:3072
	ds_read_b32 v233, v116 offset:3584
	s_waitcnt lgkmcnt(0)
	v_bfe_u32 v120, v226, 16, 1
	v_bfe_u32 v121, v227, 16, 1
	v_bfe_u32 v122, v228, 16, 1
	v_bfe_u32 v123, v229, 16, 1
	v_bfe_u32 v124, v230, 16, 1
	v_bfe_u32 v125, v231, 16, 1
	v_bfe_u32 v126, v232, 16, 1
	v_bfe_u32 v127, v233, 16, 1
	v_add3_u32 v226, v226, v120, s63
	v_add3_u32 v227, v227, v121, s63
	v_add3_u32 v228, v228, v122, s63
	v_add3_u32 v229, v229, v123, s63
	v_add3_u32 v230, v230, v124, s63
	v_add3_u32 v231, v231, v125, s63
	v_add3_u32 v232, v232, v126, s63
	v_add3_u32 v233, v233, v127, s63
	v_perm_b32 v242, v227, v226, s64
	v_perm_b32 v243, v229, v228, s64
	v_perm_b32 v244, v231, v230, s64
	v_perm_b32 v245, v233, v232, s64
	s_nop 0
	global_store_dwordx4 v93, v[242:245], s[6:7]
	ds_read_b32 v226, v118
	ds_read_b32 v227, v118 offset:512
	ds_read_b32 v228, v118 offset:1024
	ds_read_b32 v229, v118 offset:1536
	ds_read_b32 v230, v118 offset:2048
	ds_read_b32 v231, v118 offset:2560
	ds_read_b32 v232, v118 offset:3072
	ds_read_b32 v233, v118 offset:3584
	s_waitcnt lgkmcnt(0)
	v_bfe_u32 v120, v226, 16, 1
	v_bfe_u32 v121, v227, 16, 1
	v_bfe_u32 v122, v228, 16, 1
	v_bfe_u32 v123, v229, 16, 1
	v_bfe_u32 v124, v230, 16, 1
	v_bfe_u32 v125, v231, 16, 1
	v_bfe_u32 v126, v232, 16, 1
	v_bfe_u32 v127, v233, 16, 1
	v_add3_u32 v226, v226, v120, s63
	v_add3_u32 v227, v227, v121, s63
	v_add3_u32 v228, v228, v122, s63
	v_add3_u32 v229, v229, v123, s63
	v_add3_u32 v230, v230, v124, s63
	v_add3_u32 v231, v231, v125, s63
	v_add3_u32 v232, v232, v126, s63
	v_add3_u32 v233, v233, v127, s63
	v_perm_b32 v242, v227, v226, s64
	v_perm_b32 v243, v229, v228, s64
	v_perm_b32 v244, v231, v230, s64
	v_perm_b32 v245, v233, v232, s64
	s_nop 0
	global_store_dwordx4 v94, v[242:245], s[6:7]
	s_waitcnt vmcnt(14)
	v_mul_f32_e32 v176, v42, v176
	v_mul_f32_e32 v177, v42, v177
	v_mul_f32_e32 v178, v42, v178
	v_mul_f32_e32 v179, v42, v179
	ds_write_b128 v210, v[176:179]
	v_mul_f32_e32 v180, v43, v180
	v_mul_f32_e32 v181, v43, v181
	v_mul_f32_e32 v182, v43, v182
	v_mul_f32_e32 v183, v43, v183
	ds_write_b128 v210, v[180:183] offset:1024
	v_mul_f32_e32 v184, v44, v184
	v_mul_f32_e32 v185, v44, v185
	v_mul_f32_e32 v186, v44, v186
	v_mul_f32_e32 v187, v44, v187
	ds_write_b128 v210, v[184:187] offset:2048
	v_mul_f32_e32 v188, v45, v188
	v_mul_f32_e32 v189, v45, v189
	v_mul_f32_e32 v190, v45, v190
	v_mul_f32_e32 v191, v45, v191
	ds_write_b128 v210, v[188:191] offset:3072
	v_mul_f32_e32 v192, v46, v192
	v_mul_f32_e32 v193, v46, v193
	v_mul_f32_e32 v194, v46, v194
	v_mul_f32_e32 v195, v46, v195
	ds_write_b128 v210, v[192:195] offset:4096
	v_mul_f32_e32 v196, v47, v196
	v_mul_f32_e32 v197, v47, v197
	v_mul_f32_e32 v198, v47, v198
	v_mul_f32_e32 v199, v47, v199
	ds_write_b128 v210, v[196:199] offset:5120
	v_mul_f32_e32 v200, v48, v200
	v_mul_f32_e32 v201, v48, v201
	v_mul_f32_e32 v202, v48, v202
	v_mul_f32_e32 v203, v48, v203
	ds_write_b128 v210, v[200:203] offset:6144
	v_mul_f32_e32 v204, v49, v204
	v_mul_f32_e32 v205, v49, v205
	v_mul_f32_e32 v206, v49, v206
	v_mul_f32_e32 v207, v49, v207
	ds_write_b128 v210, v[204:207] offset:7168
	s_waitcnt lgkmcnt(0)
	s_barrier
; #define GAS __attribute__((address_space(1)))
; #define LAS __attribute__((address_space(3)))
; #define LDS_WAIT() asm volatile("s_waitcnt lgkmcnt(0)" ::: "memory")
; __device__ __forceinline__ unsigned pk2(float lo, float hi) { return f2bf(lo) | (f2bf(hi) << 16); }
; __device__ __forceinline__ int nat_dim(int p) { return (p >> 1) + 64 * (p & 1); }
; __device__ __forceinline__ int src_col_in(int c) {
;     if (c < 5120) { const int blk = c >> 7, p = c & 127; const bool rope = blk < 16 || ((((blk - 16) >> 2) & 1) == 0); const int d = rope ? (p >> 1) + 64 * (p & 1) : p; return blk * 128 + d; }
;     if (c < OFF_Z) return c + 2096;
;     if (c < OFF_G) return c - 4048;
;     if (c < OFF_DT) return 5120 + (c - OFF_G);
;     if (c < NSRC) return c;
;     return -1;
; template <int MAP, bool KS, bool KPERM = false>
; __device__ __forceinline__ void p0_transpose_item(const float* W, int K, int Nsrc, int nblk, bf16* WT, const float* ksA, const float* ksB, int ksplit, LAS float* scr, int item, int lane) {
;     const int kb = item / nblk, nb = item % nblk, k0 = 64 * kb, n0 = 32 * nb;
;     const int nr = n0 + (lane & 31); const int sc = MAP == 1 ? src_col_in(nr) : (MAP == 2 ? nat_dim(nr) : nr);
;     float v[32];
; #pragma unroll
;     for (int i = 0; i < 32; ++i) { const int k = k0 + 2 * i + (lane >> 5); const int ksrc = KPERM ? ((k & ~127) + nat_dim(k & 127)) : k;
;         v[i] = sc >= 0 ? W[(size_t)ksrc * Nsrc + sc] : 0.f; }
; #pragma unroll
;     for (int i = 0; i < 32; ++i) { const int kk = 2 * i + (lane >> 5); const int k = k0 + kk;
;         if (KS) v[i] *= (k < ksplit ? ksA[k] : ksB[k - ksplit]);
;         scr[kk * 33 + (lane & 31)] = v[i]; }
;     LDS_WAIT(); asm volatile("" ::: "memory");
;     const int c = lane & 7;
; #pragma unroll
;     for (int j = 0; j < 4; ++j) { const int n = (lane >> 3) + 8 * j; const LAS float* s = scr + (8 * c) * 33 + n;
;         v4u o; o.x = pk2(s[0 * 33], s[1 * 33]); o.y = pk2(s[2 * 33], s[3 * 33]); o.z = pk2(s[4 * 33], s[5 * 33]); o.w = pk2(s[6 * 33], s[7 * 33]);
;         *(GAS v4u*)(WT + (size_t)(n0 + n) * K + k0 + 8 * c) = o; }
;     LDS_WAIT(); asm volatile("" ::: "memory");
	s_add_i32 s24, s23, 24
	s_lshl_b32 s20, s24, 7
	s_cmp_lt_u32 s24, 40
	s_cselect_b32 s21, 0, 0x830
	s_cmp_lt_u32 s24, 72
	s_cselect_b32 s21, s21, 0xfffff030
	s_add_i32 s20, s20, s21
	s_lshl_b32 s20, s20, 2
	s_add_u32 s8, s46, s20
	s_addc_u32 s9, s47, 0
	global_load_dwordx4 v[176:179], v76, s[8:9]
	s_add_u32 s8, s8, 0x16280
	s_addc_u32 s9, s9, 0
	global_load_dwordx4 v[180:183], v76, s[8:9]
	s_add_u32 s8, s8, 0x16280
	s_addc_u32 s9, s9, 0
	global_load_dwordx4 v[184:187], v76, s[8:9]
	s_add_u32 s8, s8, 0x16280
	s_addc_u32 s9, s9, 0
	global_load_dwordx4 v[188:191], v76, s[8:9]
	s_add_u32 s8, s8, 0x16280
	s_addc_u32 s9, s9, 0
	global_load_dwordx4 v[192:195], v76, s[8:9]
	s_add_u32 s8, s8, 0x16280
	s_addc_u32 s9, s9, 0
	global_load_dwordx4 v[196:199], v76, s[8:9]
	s_add_u32 s8, s8, 0x16280
	s_addc_u32 s9, s9, 0
	global_load_dwordx4 v[200:203], v76, s[8:9]
	s_add_u32 s8, s8, 0x16280
	s_addc_u32 s9, s9, 0
	global_load_dwordx4 v[204:207], v76, s[8:9]
	s_add_i32 s24, s23, 8
	s_mul_i32 s20, s24, 0x100000
	s_add_u32 s6, s48, s20
	s_addc_u32 s7, s49, 0
	s_cmp_lt_u32 s24, 16
	s_cselect_b32 s20, 1, 0
	s_sub_i32 s21, s24, 16
	s_bitcmp0_b32 s21, 2
	s_cselect_b32 s21, 1, 0
	s_cmp_lt_u32 s24, 40
	s_cselect_b32 s21, s21, 0
	s_or_b32 s20, s20, s21
	s_cmp_lg_u32 s20, 0
	s_cselect_b64 s[20:21], -1, 0
	v_cndmask_b32_e64 v91, v83, v87, s[20:21]
	v_cndmask_b32_e64 v92, v84, v88, s[20:21]
	v_cndmask_b32_e64 v93, v85, v89, s[20:21]
	v_cndmask_b32_e64 v94, v86, v90, s[20:21]
	ds_read_b32 v226, v113
	ds_read_b32 v227, v113 offset:512
	ds_read_b32 v228, v113 offset:1024
	ds_read_b32 v229, v113 offset:1536
	ds_read_b32 v230, v113 offset:2048
	ds_read_b32 v231, v113 offset:2560
	ds_read_b32 v232, v113 offset:3072
	ds_read_b32 v233, v113 offset:3584
	s_waitcnt lgkmcnt(0)
	v_bfe_u32 v120, v226, 16, 1
	v_bfe_u32 v121, v227, 16, 1
	v_bfe_u32 v122, v228, 16, 1
	v_bfe_u32 v123, v229, 16, 1
	v_bfe_u32 v124, v230, 16, 1
	v_bfe_u32 v125, v231, 16, 1
	v_bfe_u32 v126, v232, 16, 1
	v_bfe_u32 v127, v233, 16, 1
	v_add3_u32 v226, v226, v120, s63
	v_add3_u32 v227, v227, v121, s63
	v_add3_u32 v228, v228, v122, s63
	v_add3_u32 v229, v229, v123, s63
	v_add3_u32 v230, v230, v124, s63
	v_add3_u32 v231, v231, v125, s63
	v_add3_u32 v232, v232, v126, s63
	v_add3_u32 v233, v233, v127, s63
	v_perm_b32 v242, v227, v226, s64
	v_perm_b32 v243, v229, v228, s64
	v_perm_b32 v244, v231, v230, s64
	v_perm_b32 v245, v233, v232, s64
	s_nop 0
	global_store_dwordx4 v91, v[242:245], s[6:7]
	ds_read_b32 v226, v115
	ds_read_b32 v227, v115 offset:512
	ds_read_b32 v228, v115 offset:1024
	ds_read_b32 v229, v115 offset:1536
	ds_read_b32 v230, v115 offset:2048
	ds_read_b32 v231, v115 offset:2560
	ds_read_b32 v232, v115 offset:3072
	ds_read_b32 v233, v115 offset:3584
	s_waitcnt lgkmcnt(0)
	v_bfe_u32 v120, v226, 16, 1
	v_bfe_u32 v121, v227, 16, 1
	v_bfe_u32 v122, v228, 16, 1
	v_bfe_u32 v123, v229, 16, 1
	v_bfe_u32 v124, v230, 16, 1
	v_bfe_u32 v125, v231, 16, 1
	v_bfe_u32 v126, v232, 16, 1
	v_bfe_u32 v127, v233, 16, 1
	v_add3_u32 v226, v226, v120, s63
	v_add3_u32 v227, v227, v121, s63
	v_add3_u32 v228, v228, v122, s63
	v_add3_u32 v229, v229, v123, s63
	v_add3_u32 v230, v230, v124, s63
	v_add3_u32 v231, v231, v125, s63
	v_add3_u32 v232, v232, v126, s63
	v_add3_u32 v233, v233, v127, s63
	v_perm_b32 v242, v227, v226, s64
	v_perm_b32 v243, v229, v228, s64
	v_perm_b32 v244, v231, v230, s64
	v_perm_b32 v245, v233, v232, s64
	s_nop 0
	global_store_dwordx4 v92, v[242:245], s[6:7]
	ds_read_b32 v226, v117
	ds_read_b32 v227, v117 offset:512
	ds_read_b32 v228, v117 offset:1024
	ds_read_b32 v229, v117 offset:1536
	ds_read_b32 v230, v117 offset:2048
	ds_read_b32 v231, v117 offset:2560
	ds_read_b32 v232, v117 offset:3072
	ds_read_b32 v233, v117 offset:3584
	s_waitcnt lgkmcnt(0)
	v_bfe_u32 v120, v226, 16, 1
	v_bfe_u32 v121, v227, 16, 1
	v_bfe_u32 v122, v228, 16, 1
	v_bfe_u32 v123, v229, 16, 1
	v_bfe_u32 v124, v230, 16, 1
	v_bfe_u32 v125, v231, 16, 1
	v_bfe_u32 v126, v232, 16, 1
	v_bfe_u32 v127, v233, 16, 1
	v_add3_u32 v226, v226, v120, s63
	v_add3_u32 v227, v227, v121, s63
	v_add3_u32 v228, v228, v122, s63
	v_add3_u32 v229, v229, v123, s63
	v_add3_u32 v230, v230, v124, s63
	v_add3_u32 v231, v231, v125, s63
	v_add3_u32 v232, v232, v126, s63
	v_add3_u32 v233, v233, v127, s63
	v_perm_b32 v242, v227, v226, s64
	v_perm_b32 v243, v229, v228, s64
	v_perm_b32 v244, v231, v230, s64
	v_perm_b32 v245, v233, v232, s64
	s_nop 0
	global_store_dwordx4 v93, v[242:245], s[6:7]
	ds_read_b32 v226, v119
	ds_read_b32 v227, v119 offset:512
	ds_read_b32 v228, v119 offset:1024
	ds_read_b32 v229, v119 offset:1536
	ds_read_b32 v230, v119 offset:2048
	ds_read_b32 v231, v119 offset:2560
	ds_read_b32 v232, v119 offset:3072
	ds_read_b32 v233, v119 offset:3584
	s_waitcnt lgkmcnt(0)
	v_bfe_u32 v120, v226, 16, 1
	v_bfe_u32 v121, v227, 16, 1
	v_bfe_u32 v122, v228, 16, 1
	v_bfe_u32 v123, v229, 16, 1
	v_bfe_u32 v124, v230, 16, 1
	v_bfe_u32 v125, v231, 16, 1
	v_bfe_u32 v126, v232, 16, 1
	v_bfe_u32 v127, v233, 16, 1
	v_add3_u32 v226, v226, v120, s63
	v_add3_u32 v227, v227, v121, s63
	v_add3_u32 v228, v228, v122, s63
	v_add3_u32 v229, v229, v123, s63
	v_add3_u32 v230, v230, v124, s63
	v_add3_u32 v231, v231, v125, s63
	v_add3_u32 v232, v232, v126, s63
	v_add3_u32 v233, v233, v127, s63
	v_perm_b32 v242, v227, v226, s64
	v_perm_b32 v243, v229, v228, s64
	v_perm_b32 v244, v231, v230, s64
	v_perm_b32 v245, v233, v232, s64
	s_nop 0
	global_store_dwordx4 v94, v[242:245], s[6:7]
	s_waitcnt vmcnt(16)
	v_mul_f32_e32 v144, v42, v144
	v_mul_f32_e32 v145, v42, v145
	v_mul_f32_e32 v146, v42, v146
	v_mul_f32_e32 v147, v42, v147
	ds_write_b128 v209, v[144:147]
	v_mul_f32_e32 v148, v43, v148
	v_mul_f32_e32 v149, v43, v149
	v_mul_f32_e32 v150, v43, v150
	v_mul_f32_e32 v151, v43, v151
	ds_write_b128 v209, v[148:151] offset:1024
	v_mul_f32_e32 v152, v44, v152
	v_mul_f32_e32 v153, v44, v153
	v_mul_f32_e32 v154, v44, v154
	v_mul_f32_e32 v155, v44, v155
	ds_write_b128 v209, v[152:155] offset:2048
	v_mul_f32_e32 v156, v45, v156
	v_mul_f32_e32 v157, v45, v157
	v_mul_f32_e32 v158, v45, v158
	v_mul_f32_e32 v159, v45, v159
	ds_write_b128 v209, v[156:159] offset:3072
	v_mul_f32_e32 v160, v46, v160
	v_mul_f32_e32 v161, v46, v161
	v_mul_f32_e32 v162, v46, v162
	v_mul_f32_e32 v163, v46, v163
	ds_write_b128 v209, v[160:163] offset:4096
	v_mul_f32_e32 v164, v47, v164
	v_mul_f32_e32 v165, v47, v165
	v_mul_f32_e32 v166, v47, v166
	v_mul_f32_e32 v167, v47, v167
	ds_write_b128 v209, v[164:167] offset:5120
	v_mul_f32_e32 v168, v48, v168
	v_mul_f32_e32 v169, v48, v169
	v_mul_f32_e32 v170, v48, v170
	v_mul_f32_e32 v171, v48, v171
	ds_write_b128 v209, v[168:171] offset:6144
	v_mul_f32_e32 v172, v49, v172
	v_mul_f32_e32 v173, v49, v173
	v_mul_f32_e32 v174, v49, v174
	v_mul_f32_e32 v175, v49, v175
	ds_write_b128 v209, v[172:175] offset:7168
	s_waitcnt lgkmcnt(0)
	s_barrier
; #define GAS __attribute__((address_space(1)))
; #define LAS __attribute__((address_space(3)))
; #define LDS_WAIT() asm volatile("s_waitcnt lgkmcnt(0)" ::: "memory")
; __device__ __forceinline__ unsigned pk2(float lo, float hi) { return f2bf(lo) | (f2bf(hi) << 16); }
; __device__ __forceinline__ int nat_dim(int p) { return (p >> 1) + 64 * (p & 1); }
; __device__ __forceinline__ int src_col_in(int c) {
;     if (c < 5120) { const int blk = c >> 7, p = c & 127; const bool rope = blk < 16 || ((((blk - 16) >> 2) & 1) == 0); const int d = rope ? (p >> 1) + 64 * (p & 1) : p; return blk * 128 + d; }
;     if (c < OFF_Z) return c + 2096;
;     if (c < OFF_G) return c - 4048;
;     if (c < OFF_DT) return 5120 + (c - OFF_G);
;     if (c < NSRC) return c;
;     return -1;
; template <int MAP, bool KS, bool KPERM = false>
; __device__ __forceinline__ void p0_transpose_item(const float* W, int K, int Nsrc, int nblk, bf16* WT, const float* ksA, const float* ksB, int ksplit, LAS float* scr, int item, int lane) {
;     const int kb = item / nblk, nb = item % nblk, k0 = 64 * kb, n0 = 32 * nb;
;     const int nr = n0 + (lane & 31); const int sc = MAP == 1 ? src_col_in(nr) : (MAP == 2 ? nat_dim(nr) : nr);
;     float v[32];
; #pragma unroll
;     for (int i = 0; i < 32; ++i) { const int k = k0 + 2 * i + (lane >> 5); const int ksrc = KPERM ? ((k & ~127) + nat_dim(k & 127)) : k;
;         v[i] = sc >= 0 ? W[(size_t)ksrc * Nsrc + sc] : 0.f; }
; #pragma unroll
;     for (int i = 0; i < 32; ++i) { const int kk = 2 * i + (lane >> 5); const int k = k0 + kk;
;         if (KS) v[i] *= (k < ksplit ? ksA[k] : ksB[k - ksplit]);
;         scr[kk * 33 + (lane & 31)] = v[i]; }
;     LDS_WAIT(); asm volatile("" ::: "memory");
;     const int c = lane & 7;
; #pragma unroll
;     for (int j = 0; j < 4; ++j) { const int n = (lane >> 3) + 8 * j; const LAS float* s = scr + (8 * c) * 33 + n;
;         v4u o; o.x = pk2(s[0 * 33], s[1 * 33]); o.y = pk2(s[2 * 33], s[3 * 33]); o.z = pk2(s[4 * 33], s[5 * 33]); o.w = pk2(s[6 * 33], s[7 * 33]);
;         *(GAS v4u*)(WT + (size_t)(n0 + n) * K + k0 + 8 * c) = o; }
;     LDS_WAIT(); asm volatile("" ::: "memory");
	s_add_i32 s24, s23, 32
	s_lshl_b32 s20, s24, 7
	s_cmp_lt_u32 s24, 40
	s_cselect_b32 s21, 0, 0x830
	s_cmp_lt_u32 s24, 72
	s_cselect_b32 s21, s21, 0xfffff030
	s_add_i32 s20, s20, s21
	s_lshl_b32 s20, s20, 2
	s_add_u32 s8, s46, s20
	s_addc_u32 s9, s47, 0
	global_load_dwordx4 v[144:147], v76, s[8:9]
	s_add_u32 s8, s8, 0x16280
	s_addc_u32 s9, s9, 0
	global_load_dwordx4 v[148:151], v76, s[8:9]
	s_add_u32 s8, s8, 0x16280
	s_addc_u32 s9, s9, 0
	global_load_dwordx4 v[152:155], v76, s[8:9]
	s_add_u32 s8, s8, 0x16280
	s_addc_u32 s9, s9, 0
	global_load_dwordx4 v[156:159], v76, s[8:9]
	s_add_u32 s8, s8, 0x16280
	s_addc_u32 s9, s9, 0
	global_load_dwordx4 v[160:163], v76, s[8:9]
	s_add_u32 s8, s8, 0x16280
	s_addc_u32 s9, s9, 0
	global_load_dwordx4 v[164:167], v76, s[8:9]
	s_add_u32 s8, s8, 0x16280
	s_addc_u32 s9, s9, 0
	global_load_dwordx4 v[168:171], v76, s[8:9]
	s_add_u32 s8, s8, 0x16280
	s_addc_u32 s9, s9, 0
	global_load_dwordx4 v[172:175], v76, s[8:9]
	s_add_i32 s24, s23, 16
	s_mul_i32 s20, s24, 0x100000
	s_add_u32 s6, s48, s20
	s_addc_u32 s7, s49, 0
	s_cmp_lt_u32 s24, 16
	s_cselect_b32 s20, 1, 0
	s_sub_i32 s21, s24, 16
	s_bitcmp0_b32 s21, 2
	s_cselect_b32 s21, 1, 0
	s_cmp_lt_u32 s24, 40
	s_cselect_b32 s21, s21, 0
	s_or_b32 s20, s20, s21
	s_cmp_lg_u32 s20, 0
	s_cselect_b64 s[20:21], -1, 0
	v_cndmask_b32_e64 v91, v83, v87, s[20:21]
	v_cndmask_b32_e64 v92, v84, v88, s[20:21]
	v_cndmask_b32_e64 v93, v85, v89, s[20:21]
	v_cndmask_b32_e64 v94, v86, v90, s[20:21]
	ds_read_b32 v226, v112
	ds_read_b32 v227, v112 offset:512
	ds_read_b32 v228, v112 offset:1024
	ds_read_b32 v229, v112 offset:1536
	ds_read_b32 v230, v112 offset:2048
	ds_read_b32 v231, v112 offset:2560
	ds_read_b32 v232, v112 offset:3072
	ds_read_b32 v233, v112 offset:3584
	s_waitcnt lgkmcnt(0)
	v_bfe_u32 v120, v226, 16, 1
	v_bfe_u32 v121, v227, 16, 1
	v_bfe_u32 v122, v228, 16, 1
	v_bfe_u32 v123, v229, 16, 1
	v_bfe_u32 v124, v230, 16, 1
	v_bfe_u32 v125, v231, 16, 1
	v_bfe_u32 v126, v232, 16, 1
	v_bfe_u32 v127, v233, 16, 1
	v_add3_u32 v226, v226, v120, s63
	v_add3_u32 v227, v227, v121, s63
	v_add3_u32 v228, v228, v122, s63
	v_add3_u32 v229, v229, v123, s63
	v_add3_u32 v230, v230, v124, s63
	v_add3_u32 v231, v231, v125, s63
	v_add3_u32 v232, v232, v126, s63
	v_add3_u32 v233, v233, v127, s63
	v_perm_b32 v242, v227, v226, s64
	v_perm_b32 v243, v229, v228, s64
	v_perm_b32 v244, v231, v230, s64
	v_perm_b32 v245, v233, v232, s64
	s_nop 0
	global_store_dwordx4 v91, v[242:245], s[6:7]
	ds_read_b32 v226, v114
	ds_read_b32 v227, v114 offset:512
	ds_read_b32 v228, v114 offset:1024
	ds_read_b32 v229, v114 offset:1536
	ds_read_b32 v230, v114 offset:2048
	ds_read_b32 v231, v114 offset:2560
	ds_read_b32 v232, v114 offset:3072
	ds_read_b32 v233, v114 offset:3584
	s_waitcnt lgkmcnt(0)
	v_bfe_u32 v120, v226, 16, 1
	v_bfe_u32 v121, v227, 16, 1
	v_bfe_u32 v122, v228, 16, 1
	v_bfe_u32 v123, v229, 16, 1
	v_bfe_u32 v124, v230, 16, 1
	v_bfe_u32 v125, v231, 16, 1
	v_bfe_u32 v126, v232, 16, 1
	v_bfe_u32 v127, v233, 16, 1
	v_add3_u32 v226, v226, v120, s63
	v_add3_u32 v227, v227, v121, s63
	v_add3_u32 v228, v228, v122, s63
	v_add3_u32 v229, v229, v123, s63
	v_add3_u32 v230, v230, v124, s63
	v_add3_u32 v231, v231, v125, s63
	v_add3_u32 v232, v232, v126, s63
	v_add3_u32 v233, v233, v127, s63
	v_perm_b32 v242, v227, v226, s64
	v_perm_b32 v243, v229, v228, s64
	v_perm_b32 v244, v231, v230, s64
	v_perm_b32 v245, v233, v232, s64
	s_nop 0
	global_store_dwordx4 v92, v[242:245], s[6:7]
	ds_read_b32 v226, v116
	ds_read_b32 v227, v116 offset:512
	ds_read_b32 v228, v116 offset:1024
	ds_read_b32 v229, v116 offset:1536
	ds_read_b32 v230, v116 offset:2048
	ds_read_b32 v231, v116 offset:2560
	ds_read_b32 v232, v116 offset:3072
	ds_read_b32 v233, v116 offset:3584
	s_waitcnt lgkmcnt(0)
	v_bfe_u32 v120, v226, 16, 1
	v_bfe_u32 v121, v227, 16, 1
	v_bfe_u32 v122, v228, 16, 1
	v_bfe_u32 v123, v229, 16, 1
	v_bfe_u32 v124, v230, 16, 1
	v_bfe_u32 v125, v231, 16, 1
	v_bfe_u32 v126, v232, 16, 1
	v_bfe_u32 v127, v233, 16, 1
	v_add3_u32 v226, v226, v120, s63
	v_add3_u32 v227, v227, v121, s63
	v_add3_u32 v228, v228, v122, s63
	v_add3_u32 v229, v229, v123, s63
	v_add3_u32 v230, v230, v124, s63
	v_add3_u32 v231, v231, v125, s63
	v_add3_u32 v232, v232, v126, s63
	v_add3_u32 v233, v233, v127, s63
	v_perm_b32 v242, v227, v226, s64
	v_perm_b32 v243, v229, v228, s64
	v_perm_b32 v244, v231, v230, s64
	v_perm_b32 v245, v233, v232, s64
	s_nop 0
	global_store_dwordx4 v93, v[242:245], s[6:7]
	ds_read_b32 v226, v118
	ds_read_b32 v227, v118 offset:512
	ds_read_b32 v228, v118 offset:1024
	ds_read_b32 v229, v118 offset:1536
	ds_read_b32 v230, v118 offset:2048
	ds_read_b32 v231, v118 offset:2560
	ds_read_b32 v232, v118 offset:3072
	ds_read_b32 v233, v118 offset:3584
	s_waitcnt lgkmcnt(0)
	v_bfe_u32 v120, v226, 16, 1
	v_bfe_u32 v121, v227, 16, 1
	v_bfe_u32 v122, v228, 16, 1
	v_bfe_u32 v123, v229, 16, 1
	v_bfe_u32 v124, v230, 16, 1
	v_bfe_u32 v125, v231, 16, 1
	v_bfe_u32 v126, v232, 16, 1
	v_bfe_u32 v127, v233, 16, 1
	v_add3_u32 v226, v226, v120, s63
	v_add3_u32 v227, v227, v121, s63
	v_add3_u32 v228, v228, v122, s63
	v_add3_u32 v229, v229, v123, s63
	v_add3_u32 v230, v230, v124, s63
	v_add3_u32 v231, v231, v125, s63
	v_add3_u32 v232, v232, v126, s63
	v_add3_u32 v233, v233, v127, s63
	v_perm_b32 v242, v227, v226, s64
	v_perm_b32 v243, v229, v228, s64
	v_perm_b32 v244, v231, v230, s64
	v_perm_b32 v245, v233, v232, s64
	s_nop 0
	global_store_dwordx4 v94, v[242:245], s[6:7]
	s_waitcnt vmcnt(16)
	v_mul_f32_e32 v176, v42, v176
	v_mul_f32_e32 v177, v42, v177
	v_mul_f32_e32 v178, v42, v178
	v_mul_f32_e32 v179, v42, v179
	ds_write_b128 v210, v[176:179]
	v_mul_f32_e32 v180, v43, v180
	v_mul_f32_e32 v181, v43, v181
	v_mul_f32_e32 v182, v43, v182
	v_mul_f32_e32 v183, v43, v183
	ds_write_b128 v210, v[180:183] offset:1024
	v_mul_f32_e32 v184, v44, v184
	v_mul_f32_e32 v185, v44, v185
	v_mul_f32_e32 v186, v44, v186
	v_mul_f32_e32 v187, v44, v187
	ds_write_b128 v210, v[184:187] offset:2048
	v_mul_f32_e32 v188, v45, v188
	v_mul_f32_e32 v189, v45, v189
	v_mul_f32_e32 v190, v45, v190
	v_mul_f32_e32 v191, v45, v191
	ds_write_b128 v210, v[188:191] offset:3072
	v_mul_f32_e32 v192, v46, v192
	v_mul_f32_e32 v193, v46, v193
	v_mul_f32_e32 v194, v46, v194
	v_mul_f32_e32 v195, v46, v195
	ds_write_b128 v210, v[192:195] offset:4096
	v_mul_f32_e32 v196, v47, v196
	v_mul_f32_e32 v197, v47, v197
	v_mul_f32_e32 v198, v47, v198
	v_mul_f32_e32 v199, v47, v199
	ds_write_b128 v210, v[196:199] offset:5120
	v_mul_f32_e32 v200, v48, v200
	v_mul_f32_e32 v201, v48, v201
	v_mul_f32_e32 v202, v48, v202
	v_mul_f32_e32 v203, v48, v203
	ds_write_b128 v210, v[200:203] offset:6144
	v_mul_f32_e32 v204, v49, v204
	v_mul_f32_e32 v205, v49, v205
	v_mul_f32_e32 v206, v49, v206
	v_mul_f32_e32 v207, v49, v207
	ds_write_b128 v210, v[204:207] offset:7168
	s_waitcnt lgkmcnt(0)
	s_barrier
; #define GAS __attribute__((address_space(1)))
; #define LAS __attribute__((address_space(3)))
; #define LDS_WAIT() asm volatile("s_waitcnt lgkmcnt(0)" ::: "memory")
; __device__ __forceinline__ unsigned pk2(float lo, float hi) { return f2bf(lo) | (f2bf(hi) << 16); }
; __device__ __forceinline__ int nat_dim(int p) { return (p >> 1) + 64 * (p & 1); }
; __device__ __forceinline__ int src_col_in(int c) {
;     if (c < 5120) { const int blk = c >> 7, p = c & 127; const bool rope = blk < 16 || ((((blk - 16) >> 2) & 1) == 0); const int d = rope ? (p >> 1) + 64 * (p & 1) : p; return blk * 128 + d; }
;     if (c < OFF_Z) return c + 2096;
;     if (c < OFF_G) return c - 4048;
;     if (c < OFF_DT) return 5120 + (c - OFF_G);
;     if (c < NSRC) return c;
;     return -1;
; template <int MAP, bool KS, bool KPERM = false>
; __device__ __forceinline__ void p0_transpose_item(const float* W, int K, int Nsrc, int nblk, bf16* WT, const float* ksA, const float* ksB, int ksplit, LAS float* scr, int item, int lane) {
;     const int kb = item / nblk, nb = item % nblk, k0 = 64 * kb, n0 = 32 * nb;
;     const int nr = n0 + (lane & 31); const int sc = MAP == 1 ? src_col_in(nr) : (MAP == 2 ? nat_dim(nr) : nr);
;     float v[32];
; #pragma unroll
;     for (int i = 0; i < 32; ++i) { const int k = k0 + 2 * i + (lane >> 5); const int ksrc = KPERM ? ((k & ~127) + nat_dim(k & 127)) : k;
;         v[i] = sc >= 0 ? W[(size_t)ksrc * Nsrc + sc] : 0.f; }
; #pragma unroll
;     for (int i = 0; i < 32; ++i) { const int kk = 2 * i + (lane >> 5); const int k = k0 + kk;
;         if (KS) v[i] *= (k < ksplit ? ksA[k] : ksB[k - ksplit]);
;         scr[kk * 33 + (lane & 31)] = v[i]; }
;     LDS_WAIT(); asm volatile("" ::: "memory");
;     const int c = lane & 7;
; #pragma unroll
;     for (int j = 0; j < 4; ++j) { const int n = (lane >> 3) + 8 * j; const LAS float* s = scr + (8 * c) * 33 + n;
;         v4u o; o.x = pk2(s[0 * 33], s[1 * 33]); o.y = pk2(s[2 * 33], s[3 * 33]); o.z = pk2(s[4 * 33], s[5 * 33]); o.w = pk2(s[6 * 33], s[7 * 33]);
;         *(GAS v4u*)(WT + (size_t)(n0 + n) * K + k0 + 8 * c) = o; }
;     LDS_WAIT(); asm volatile("" ::: "memory");
	s_add_i32 s24, s23, 40
	s_lshl_b32 s20, s24, 7
	s_cmp_lt_u32 s24, 40
	s_cselect_b32 s21, 0, 0x830
	s_cmp_lt_u32 s24, 72
	s_cselect_b32 s21, s21, 0xfffff030
	s_add_i32 s20, s20, s21
	s_lshl_b32 s20, s20, 2
	s_add_u32 s8, s46, s20
	s_addc_u32 s9, s47, 0
	global_load_dwordx4 v[176:179], v76, s[8:9]
	s_add_u32 s8, s8, 0x16280
	s_addc_u32 s9, s9, 0
	global_load_dwordx4 v[180:183], v76, s[8:9]
	s_add_u32 s8, s8, 0x16280
	s_addc_u32 s9, s9, 0
	global_load_dwordx4 v[184:187], v76, s[8:9]
	s_add_u32 s8, s8, 0x16280
	s_addc_u32 s9, s9, 0
	global_load_dwordx4 v[188:191], v76, s[8:9]
	s_add_u32 s8, s8, 0x16280
	s_addc_u32 s9, s9, 0
	global_load_dwordx4 v[192:195], v76, s[8:9]
	s_add_u32 s8, s8, 0x16280
	s_addc_u32 s9, s9, 0
	global_load_dwordx4 v[196:199], v76, s[8:9]
	s_add_u32 s8, s8, 0x16280
	s_addc_u32 s9, s9, 0
	global_load_dwordx4 v[200:203], v76, s[8:9]
	s_add_u32 s8, s8, 0x16280
	s_addc_u32 s9, s9, 0
	global_load_dwordx4 v[204:207], v76, s[8:9]
	s_add_i32 s24, s23, 24
	s_mul_i32 s20, s24, 0x100000
	s_add_u32 s6, s48, s20
	s_addc_u32 s7, s49, 0
	s_cmp_lt_u32 s24, 16
	s_cselect_b32 s20, 1, 0
	s_sub_i32 s21, s24, 16
	s_bitcmp0_b32 s21, 2
	s_cselect_b32 s21, 1, 0
	s_cmp_lt_u32 s24, 40
	s_cselect_b32 s21, s21, 0
	s_or_b32 s20, s20, s21
	s_cmp_lg_u32 s20, 0
	s_cselect_b64 s[20:21], -1, 0
	v_cndmask_b32_e64 v91, v83, v87, s[20:21]
	v_cndmask_b32_e64 v92, v84, v88, s[20:21]
	v_cndmask_b32_e64 v93, v85, v89, s[20:21]
	v_cndmask_b32_e64 v94, v86, v90, s[20:21]
	ds_read_b32 v226, v113
	ds_read_b32 v227, v113 offset:512
	ds_read_b32 v228, v113 offset:1024
	ds_read_b32 v229, v113 offset:1536
	ds_read_b32 v230, v113 offset:2048
	ds_read_b32 v231, v113 offset:2560
	ds_read_b32 v232, v113 offset:3072
	ds_read_b32 v233, v113 offset:3584
	s_waitcnt lgkmcnt(0)
	v_bfe_u32 v120, v226, 16, 1
	v_bfe_u32 v121, v227, 16, 1
	v_bfe_u32 v122, v228, 16, 1
	v_bfe_u32 v123, v229, 16, 1
	v_bfe_u32 v124, v230, 16, 1
	v_bfe_u32 v125, v231, 16, 1
	v_bfe_u32 v126, v232, 16, 1
	v_bfe_u32 v127, v233, 16, 1
	v_add3_u32 v226, v226, v120, s63
	v_add3_u32 v227, v227, v121, s63
	v_add3_u32 v228, v228, v122, s63
	v_add3_u32 v229, v229, v123, s63
	v_add3_u32 v230, v230, v124, s63
	v_add3_u32 v231, v231, v125, s63
	v_add3_u32 v232, v232, v126, s63
	v_add3_u32 v233, v233, v127, s63
	v_perm_b32 v242, v227, v226, s64
	v_perm_b32 v243, v229, v228, s64
	v_perm_b32 v244, v231, v230, s64
	v_perm_b32 v245, v233, v232, s64
	s_nop 0
	global_store_dwordx4 v91, v[242:245], s[6:7]
	ds_read_b32 v226, v115
	ds_read_b32 v227, v115 offset:512
	ds_read_b32 v228, v115 offset:1024
	ds_read_b32 v229, v115 offset:1536
	ds_read_b32 v230, v115 offset:2048
	ds_read_b32 v231, v115 offset:2560
	ds_read_b32 v232, v115 offset:3072
	ds_read_b32 v233, v115 offset:3584
	s_waitcnt lgkmcnt(0)
	v_bfe_u32 v120, v226, 16, 1
	v_bfe_u32 v121, v227, 16, 1
	v_bfe_u32 v122, v228, 16, 1
	v_bfe_u32 v123, v229, 16, 1
	v_bfe_u32 v124, v230, 16, 1
	v_bfe_u32 v125, v231, 16, 1
	v_bfe_u32 v126, v232, 16, 1
	v_bfe_u32 v127, v233, 16, 1
	v_add3_u32 v226, v226, v120, s63
	v_add3_u32 v227, v227, v121, s63
	v_add3_u32 v228, v228, v122, s63
	v_add3_u32 v229, v229, v123, s63
	v_add3_u32 v230, v230, v124, s63
	v_add3_u32 v231, v231, v125, s63
	v_add3_u32 v232, v232, v126, s63
	v_add3_u32 v233, v233, v127, s63
	v_perm_b32 v242, v227, v226, s64
	v_perm_b32 v243, v229, v228, s64
	v_perm_b32 v244, v231, v230, s64
	v_perm_b32 v245, v233, v232, s64
	s_nop 0
	global_store_dwordx4 v92, v[242:245], s[6:7]
	ds_read_b32 v226, v117
	ds_read_b32 v227, v117 offset:512
	ds_read_b32 v228, v117 offset:1024
	ds_read_b32 v229, v117 offset:1536
	ds_read_b32 v230, v117 offset:2048
	ds_read_b32 v231, v117 offset:2560
	ds_read_b32 v232, v117 offset:3072
	ds_read_b32 v233, v117 offset:3584
	s_waitcnt lgkmcnt(0)
	v_bfe_u32 v120, v226, 16, 1
	v_bfe_u32 v121, v227, 16, 1
	v_bfe_u32 v122, v228, 16, 1
	v_bfe_u32 v123, v229, 16, 1
	v_bfe_u32 v124, v230, 16, 1
	v_bfe_u32 v125, v231, 16, 1
	v_bfe_u32 v126, v232, 16, 1
	v_bfe_u32 v127, v233, 16, 1
	v_add3_u32 v226, v226, v120, s63
	v_add3_u32 v227, v227, v121, s63
	v_add3_u32 v228, v228, v122, s63
	v_add3_u32 v229, v229, v123, s63
	v_add3_u32 v230, v230, v124, s63
	v_add3_u32 v231, v231, v125, s63
	v_add3_u32 v232, v232, v126, s63
	v_add3_u32 v233, v233, v127, s63
	v_perm_b32 v242, v227, v226, s64
	v_perm_b32 v243, v229, v228, s64
	v_perm_b32 v244, v231, v230, s64
	v_perm_b32 v245, v233, v232, s64
	s_nop 0
	global_store_dwordx4 v93, v[242:245], s[6:7]
	ds_read_b32 v226, v119
	ds_read_b32 v227, v119 offset:512
	ds_read_b32 v228, v119 offset:1024
	ds_read_b32 v229, v119 offset:1536
	ds_read_b32 v230, v119 offset:2048
	ds_read_b32 v231, v119 offset:2560
	ds_read_b32 v232, v119 offset:3072
	ds_read_b32 v233, v119 offset:3584
	s_waitcnt lgkmcnt(0)
	v_bfe_u32 v120, v226, 16, 1
	v_bfe_u32 v121, v227, 16, 1
	v_bfe_u32 v122, v228, 16, 1
	v_bfe_u32 v123, v229, 16, 1
	v_bfe_u32 v124, v230, 16, 1
	v_bfe_u32 v125, v231, 16, 1
	v_bfe_u32 v126, v232, 16, 1
	v_bfe_u32 v127, v233, 16, 1
	v_add3_u32 v226, v226, v120, s63
	v_add3_u32 v227, v227, v121, s63
	v_add3_u32 v228, v228, v122, s63
	v_add3_u32 v229, v229, v123, s63
	v_add3_u32 v230, v230, v124, s63
	v_add3_u32 v231, v231, v125, s63
	v_add3_u32 v232, v232, v126, s63
	v_add3_u32 v233, v233, v127, s63
	v_perm_b32 v242, v227, v226, s64
	v_perm_b32 v243, v229, v228, s64
	v_perm_b32 v244, v231, v230, s64
	v_perm_b32 v245, v233, v232, s64
	s_nop 0
	global_store_dwordx4 v94, v[242:245], s[6:7]
	s_waitcnt vmcnt(16)
	v_mul_f32_e32 v144, v42, v144
	v_mul_f32_e32 v145, v42, v145
	v_mul_f32_e32 v146, v42, v146
	v_mul_f32_e32 v147, v42, v147
	ds_write_b128 v209, v[144:147]
	v_mul_f32_e32 v148, v43, v148
	v_mul_f32_e32 v149, v43, v149
	v_mul_f32_e32 v150, v43, v150
	v_mul_f32_e32 v151, v43, v151
	ds_write_b128 v209, v[148:151] offset:1024
	v_mul_f32_e32 v152, v44, v152
	v_mul_f32_e32 v153, v44, v153
	v_mul_f32_e32 v154, v44, v154
	v_mul_f32_e32 v155, v44, v155
	ds_write_b128 v209, v[152:155] offset:2048
	v_mul_f32_e32 v156, v45, v156
	v_mul_f32_e32 v157, v45, v157
	v_mul_f32_e32 v158, v45, v158
	v_mul_f32_e32 v159, v45, v159
	ds_write_b128 v209, v[156:159] offset:3072
	v_mul_f32_e32 v160, v46, v160
	v_mul_f32_e32 v161, v46, v161
	v_mul_f32_e32 v162, v46, v162
	v_mul_f32_e32 v163, v46, v163
	ds_write_b128 v209, v[160:163] offset:4096
	v_mul_f32_e32 v164, v47, v164
	v_mul_f32_e32 v165, v47, v165
	v_mul_f32_e32 v166, v47, v166
	v_mul_f32_e32 v167, v47, v167
	ds_write_b128 v209, v[164:167] offset:5120
	v_mul_f32_e32 v168, v48, v168
	v_mul_f32_e32 v169, v48, v169
	v_mul_f32_e32 v170, v48, v170
	v_mul_f32_e32 v171, v48, v171
	ds_write_b128 v209, v[168:171] offset:6144
	v_mul_f32_e32 v172, v49, v172
	v_mul_f32_e32 v173, v49, v173
	v_mul_f32_e32 v174, v49, v174
	v_mul_f32_e32 v175, v49, v175
	ds_write_b128 v209, v[172:175] offset:7168
	s_waitcnt lgkmcnt(0)
	s_barrier
; #define GAS __attribute__((address_space(1)))
; #define LAS __attribute__((address_space(3)))
; #define LDS_WAIT() asm volatile("s_waitcnt lgkmcnt(0)" ::: "memory")
; __device__ __forceinline__ unsigned pk2(float lo, float hi) { return f2bf(lo) | (f2bf(hi) << 16); }
; __device__ __forceinline__ int nat_dim(int p) { return (p >> 1) + 64 * (p & 1); }
; __device__ __forceinline__ int src_col_in(int c) {
;     if (c < 5120) { const int blk = c >> 7, p = c & 127; const bool rope = blk < 16 || ((((blk - 16) >> 2) & 1) == 0); const int d = rope ? (p >> 1) + 64 * (p & 1) : p; return blk * 128 + d; }
;     if (c < OFF_Z) return c + 2096;
;     if (c < OFF_G) return c - 4048;
;     if (c < OFF_DT) return 5120 + (c - OFF_G);
;     if (c < NSRC) return c;
;     return -1;
; template <int MAP, bool KS, bool KPERM = false>
; __device__ __forceinline__ void p0_transpose_item(const float* W, int K, int Nsrc, int nblk, bf16* WT, const float* ksA, const float* ksB, int ksplit, LAS float* scr, int item, int lane) {
;     const int kb = item / nblk, nb = item % nblk, k0 = 64 * kb, n0 = 32 * nb;
;     const int nr = n0 + (lane & 31); const int sc = MAP == 1 ? src_col_in(nr) : (MAP == 2 ? nat_dim(nr) : nr);
;     float v[32];
; #pragma unroll
;     for (int i = 0; i < 32; ++i) { const int k = k0 + 2 * i + (lane >> 5); const int ksrc = KPERM ? ((k & ~127) + nat_dim(k & 127)) : k;
;         v[i] = sc >= 0 ? W[(size_t)ksrc * Nsrc + sc] : 0.f; }
; #pragma unroll
;     for (int i = 0; i < 32; ++i) { const int kk = 2 * i + (lane >> 5); const int k = k0 + kk;
;         if (KS) v[i] *= (k < ksplit ? ksA[k] : ksB[k - ksplit]);
;         scr[kk * 33 + (lane & 31)] = v[i]; }
;     LDS_WAIT(); asm volatile("" ::: "memory");
;     const int c = lane & 7;
; #pragma unroll
;     for (int j = 0; j < 4; ++j) { const int n = (lane >> 3) + 8 * j; const LAS float* s = scr + (8 * c) * 33 + n;
;         v4u o; o.x = pk2(s[0 * 33], s[1 * 33]); o.y = pk2(s[2 * 33], s[3 * 33]); o.z = pk2(s[4 * 33], s[5 * 33]); o.w = pk2(s[6 * 33], s[7 * 33]);
;         *(GAS v4u*)(WT + (size_t)(n0 + n) * K + k0 + 8 * c) = o; }
;     LDS_WAIT(); asm volatile("" ::: "memory");
	s_add_i32 s24, s23, 48
	s_lshl_b32 s20, s24, 7
	s_cmp_lt_u32 s24, 40
	s_cselect_b32 s21, 0, 0x830
	s_cmp_lt_u32 s24, 72
	s_cselect_b32 s21, s21, 0xfffff030
	s_add_i32 s20, s20, s21
	s_lshl_b32 s20, s20, 2
	s_add_u32 s8, s46, s20
	s_addc_u32 s9, s47, 0
	global_load_dwordx4 v[144:147], v76, s[8:9]
	s_add_u32 s8, s8, 0x16280
	s_addc_u32 s9, s9, 0
	global_load_dwordx4 v[148:151], v76, s[8:9]
	s_add_u32 s8, s8, 0x16280
	s_addc_u32 s9, s9, 0
	global_load_dwordx4 v[152:155], v76, s[8:9]
	s_add_u32 s8, s8, 0x16280
	s_addc_u32 s9, s9, 0
	global_load_dwordx4 v[156:159], v76, s[8:9]
	s_add_u32 s8, s8, 0x16280
	s_addc_u32 s9, s9, 0
	global_load_dwordx4 v[160:163], v76, s[8:9]
	s_add_u32 s8, s8, 0x16280
	s_addc_u32 s9, s9, 0
	global_load_dwordx4 v[164:167], v76, s[8:9]
	s_add_u32 s8, s8, 0x16280
	s_addc_u32 s9, s9, 0
	global_load_dwordx4 v[168:171], v76, s[8:9]
	s_add_u32 s8, s8, 0x16280
	s_addc_u32 s9, s9, 0
	global_load_dwordx4 v[172:175], v76, s[8:9]
	s_add_i32 s24, s23, 32
	s_mul_i32 s20, s24, 0x100000
	s_add_u32 s6, s48, s20
	s_addc_u32 s7, s49, 0
	s_cmp_lt_u32 s24, 16
	s_cselect_b32 s20, 1, 0
	s_sub_i32 s21, s24, 16
	s_bitcmp0_b32 s21, 2
	s_cselect_b32 s21, 1, 0
	s_cmp_lt_u32 s24, 40
	s_cselect_b32 s21, s21, 0
	s_or_b32 s20, s20, s21
	s_cmp_lg_u32 s20, 0
	s_cselect_b64 s[20:21], -1, 0
	v_cndmask_b32_e64 v91, v83, v87, s[20:21]
	v_cndmask_b32_e64 v92, v84, v88, s[20:21]
	v_cndmask_b32_e64 v93, v85, v89, s[20:21]
	v_cndmask_b32_e64 v94, v86, v90, s[20:21]
	ds_read_b32 v226, v112
	ds_read_b32 v227, v112 offset:512
	ds_read_b32 v228, v112 offset:1024
	ds_read_b32 v229, v112 offset:1536
	ds_read_b32 v230, v112 offset:2048
	ds_read_b32 v231, v112 offset:2560
	ds_read_b32 v232, v112 offset:3072
	ds_read_b32 v233, v112 offset:3584
	s_waitcnt lgkmcnt(0)
	v_bfe_u32 v120, v226, 16, 1
	v_bfe_u32 v121, v227, 16, 1
	v_bfe_u32 v122, v228, 16, 1
	v_bfe_u32 v123, v229, 16, 1
	v_bfe_u32 v124, v230, 16, 1
	v_bfe_u32 v125, v231, 16, 1
	v_bfe_u32 v126, v232, 16, 1
	v_bfe_u32 v127, v233, 16, 1
	v_add3_u32 v226, v226, v120, s63
	v_add3_u32 v227, v227, v121, s63
	v_add3_u32 v228, v228, v122, s63
	v_add3_u32 v229, v229, v123, s63
	v_add3_u32 v230, v230, v124, s63
	v_add3_u32 v231, v231, v125, s63
	v_add3_u32 v232, v232, v126, s63
	v_add3_u32 v233, v233, v127, s63
	v_perm_b32 v242, v227, v226, s64
	v_perm_b32 v243, v229, v228, s64
	v_perm_b32 v244, v231, v230, s64
	v_perm_b32 v245, v233, v232, s64
	s_nop 0
	global_store_dwordx4 v91, v[242:245], s[6:7]
	ds_read_b32 v226, v114
	ds_read_b32 v227, v114 offset:512
	ds_read_b32 v228, v114 offset:1024
	ds_read_b32 v229, v114 offset:1536
	ds_read_b32 v230, v114 offset:2048
	ds_read_b32 v231, v114 offset:2560
	ds_read_b32 v232, v114 offset:3072
	ds_read_b32 v233, v114 offset:3584
	s_waitcnt lgkmcnt(0)
	v_bfe_u32 v120, v226, 16, 1
	v_bfe_u32 v121, v227, 16, 1
	v_bfe_u32 v122, v228, 16, 1
	v_bfe_u32 v123, v229, 16, 1
	v_bfe_u32 v124, v230, 16, 1
	v_bfe_u32 v125, v231, 16, 1
	v_bfe_u32 v126, v232, 16, 1
	v_bfe_u32 v127, v233, 16, 1
	v_add3_u32 v226, v226, v120, s63
	v_add3_u32 v227, v227, v121, s63
	v_add3_u32 v228, v228, v122, s63
	v_add3_u32 v229, v229, v123, s63
	v_add3_u32 v230, v230, v124, s63
	v_add3_u32 v231, v231, v125, s63
	v_add3_u32 v232, v232, v126, s63
	v_add3_u32 v233, v233, v127, s63
	v_perm_b32 v242, v227, v226, s64
	v_perm_b32 v243, v229, v228, s64
	v_perm_b32 v244, v231, v230, s64
	v_perm_b32 v245, v233, v232, s64
	s_nop 0
	global_store_dwordx4 v92, v[242:245], s[6:7]
	ds_read_b32 v226, v116
	ds_read_b32 v227, v116 offset:512
	ds_read_b32 v228, v116 offset:1024
	ds_read_b32 v229, v116 offset:1536
	ds_read_b32 v230, v116 offset:2048
	ds_read_b32 v231, v116 offset:2560
	ds_read_b32 v232, v116 offset:3072
	ds_read_b32 v233, v116 offset:3584
	s_waitcnt lgkmcnt(0)
	v_bfe_u32 v120, v226, 16, 1
	v_bfe_u32 v121, v227, 16, 1
	v_bfe_u32 v122, v228, 16, 1
	v_bfe_u32 v123, v229, 16, 1
	v_bfe_u32 v124, v230, 16, 1
	v_bfe_u32 v125, v231, 16, 1
	v_bfe_u32 v126, v232, 16, 1
	v_bfe_u32 v127, v233, 16, 1
	v_add3_u32 v226, v226, v120, s63
	v_add3_u32 v227, v227, v121, s63
	v_add3_u32 v228, v228, v122, s63
	v_add3_u32 v229, v229, v123, s63
	v_add3_u32 v230, v230, v124, s63
	v_add3_u32 v231, v231, v125, s63
	v_add3_u32 v232, v232, v126, s63
	v_add3_u32 v233, v233, v127, s63
	v_perm_b32 v242, v227, v226, s64
	v_perm_b32 v243, v229, v228, s64
	v_perm_b32 v244, v231, v230, s64
	v_perm_b32 v245, v233, v232, s64
	s_nop 0
	global_store_dwordx4 v93, v[242:245], s[6:7]
	ds_read_b32 v226, v118
	ds_read_b32 v227, v118 offset:512
	ds_read_b32 v228, v118 offset:1024
	ds_read_b32 v229, v118 offset:1536
	ds_read_b32 v230, v118 offset:2048
	ds_read_b32 v231, v118 offset:2560
	ds_read_b32 v232, v118 offset:3072
	ds_read_b32 v233, v118 offset:3584
	s_waitcnt lgkmcnt(0)
	v_bfe_u32 v120, v226, 16, 1
	v_bfe_u32 v121, v227, 16, 1
	v_bfe_u32 v122, v228, 16, 1
	v_bfe_u32 v123, v229, 16, 1
	v_bfe_u32 v124, v230, 16, 1
	v_bfe_u32 v125, v231, 16, 1
	v_bfe_u32 v126, v232, 16, 1
	v_bfe_u32 v127, v233, 16, 1
	v_add3_u32 v226, v226, v120, s63
	v_add3_u32 v227, v227, v121, s63
	v_add3_u32 v228, v228, v122, s63
	v_add3_u32 v229, v229, v123, s63
	v_add3_u32 v230, v230, v124, s63
	v_add3_u32 v231, v231, v125, s63
	v_add3_u32 v232, v232, v126, s63
	v_add3_u32 v233, v233, v127, s63
	v_perm_b32 v242, v227, v226, s64
	v_perm_b32 v243, v229, v228, s64
	v_perm_b32 v244, v231, v230, s64
	v_perm_b32 v245, v233, v232, s64
	s_nop 0
	global_store_dwordx4 v94, v[242:245], s[6:7]
	s_waitcnt vmcnt(16)
	v_mul_f32_e32 v176, v42, v176
	v_mul_f32_e32 v177, v42, v177
	v_mul_f32_e32 v178, v42, v178
	v_mul_f32_e32 v179, v42, v179
	ds_write_b128 v210, v[176:179]
	v_mul_f32_e32 v180, v43, v180
	v_mul_f32_e32 v181, v43, v181
	v_mul_f32_e32 v182, v43, v182
	v_mul_f32_e32 v183, v43, v183
	ds_write_b128 v210, v[180:183] offset:1024
	v_mul_f32_e32 v184, v44, v184
	v_mul_f32_e32 v185, v44, v185
	v_mul_f32_e32 v186, v44, v186
	v_mul_f32_e32 v187, v44, v187
	ds_write_b128 v210, v[184:187] offset:2048
	v_mul_f32_e32 v188, v45, v188
	v_mul_f32_e32 v189, v45, v189
	v_mul_f32_e32 v190, v45, v190
	v_mul_f32_e32 v191, v45, v191
	ds_write_b128 v210, v[188:191] offset:3072
	v_mul_f32_e32 v192, v46, v192
	v_mul_f32_e32 v193, v46, v193
	v_mul_f32_e32 v194, v46, v194
	v_mul_f32_e32 v195, v46, v195
	ds_write_b128 v210, v[192:195] offset:4096
	v_mul_f32_e32 v196, v47, v196
	v_mul_f32_e32 v197, v47, v197
	v_mul_f32_e32 v198, v47, v198
	v_mul_f32_e32 v199, v47, v199
	ds_write_b128 v210, v[196:199] offset:5120
	v_mul_f32_e32 v200, v48, v200
	v_mul_f32_e32 v201, v48, v201
	v_mul_f32_e32 v202, v48, v202
	v_mul_f32_e32 v203, v48, v203
	ds_write_b128 v210, v[200:203] offset:6144
	v_mul_f32_e32 v204, v49, v204
	v_mul_f32_e32 v205, v49, v205
	v_mul_f32_e32 v206, v49, v206
	v_mul_f32_e32 v207, v49, v207
	ds_write_b128 v210, v[204:207] offset:7168
	s_waitcnt lgkmcnt(0)
	s_barrier
; #define GAS __attribute__((address_space(1)))
; #define LAS __attribute__((address_space(3)))
; #define LDS_WAIT() asm volatile("s_waitcnt lgkmcnt(0)" ::: "memory")
; __device__ __forceinline__ unsigned pk2(float lo, float hi) { return f2bf(lo) | (f2bf(hi) << 16); }
; __device__ __forceinline__ int nat_dim(int p) { return (p >> 1) + 64 * (p & 1); }
; __device__ __forceinline__ int src_col_in(int c) {
;     if (c < 5120) { const int blk = c >> 7, p = c & 127; const bool rope = blk < 16 || ((((blk - 16) >> 2) & 1) == 0); const int d = rope ? (p >> 1) + 64 * (p & 1) : p; return blk * 128 + d; }
;     if (c < OFF_Z) return c + 2096;
;     if (c < OFF_G) return c - 4048;
;     if (c < OFF_DT) return 5120 + (c - OFF_G);
;     if (c < NSRC) return c;
;     return -1;
; template <int MAP, bool KS, bool KPERM = false>
; __device__ __forceinline__ void p0_transpose_item(const float* W, int K, int Nsrc, int nblk, bf16* WT, const float* ksA, const float* ksB, int ksplit, LAS float* scr, int item, int lane) {
;     const int kb = item / nblk, nb = item % nblk, k0 = 64 * kb, n0 = 32 * nb;
;     const int nr = n0 + (lane & 31); const int sc = MAP == 1 ? src_col_in(nr) : (MAP == 2 ? nat_dim(nr) : nr);
;     float v[32];
; #pragma unroll
;     for (int i = 0; i < 32; ++i) { const int k = k0 + 2 * i + (lane >> 5); const int ksrc = KPERM ? ((k & ~127) + nat_dim(k & 127)) : k;
;         v[i] = sc >= 0 ? W[(size_t)ksrc * Nsrc + sc] : 0.f; }
; #pragma unroll
;     for (int i = 0; i < 32; ++i) { const int kk = 2 * i + (lane >> 5); const int k = k0 + kk;
;         if (KS) v[i] *= (k < ksplit ? ksA[k] : ksB[k - ksplit]);
;         scr[kk * 33 + (lane & 31)] = v[i]; }
;     LDS_WAIT(); asm volatile("" ::: "memory");
;     const int c = lane & 7;
; #pragma unroll
;     for (int j = 0; j < 4; ++j) { const int n = (lane >> 3) + 8 * j; const LAS float* s = scr + (8 * c) * 33 + n;
;         v4u o; o.x = pk2(s[0 * 33], s[1 * 33]); o.y = pk2(s[2 * 33], s[3 * 33]); o.z = pk2(s[4 * 33], s[5 * 33]); o.w = pk2(s[6 * 33], s[7 * 33]);
;         *(GAS v4u*)(WT + (size_t)(n0 + n) * K + k0 + 8 * c) = o; }
;     LDS_WAIT(); asm volatile("" ::: "memory");
	s_add_i32 s24, s23, 56
	s_lshl_b32 s20, s24, 7
	s_cmp_lt_u32 s24, 40
	s_cselect_b32 s21, 0, 0x830
	s_cmp_lt_u32 s24, 72
	s_cselect_b32 s21, s21, 0xfffff030
	s_add_i32 s20, s20, s21
	s_lshl_b32 s20, s20, 2
	s_add_u32 s8, s46, s20
	s_addc_u32 s9, s47, 0
	global_load_dwordx4 v[176:179], v76, s[8:9]
	s_add_u32 s8, s8, 0x16280
	s_addc_u32 s9, s9, 0
	global_load_dwordx4 v[180:183], v76, s[8:9]
	s_add_u32 s8, s8, 0x16280
	s_addc_u32 s9, s9, 0
	global_load_dwordx4 v[184:187], v76, s[8:9]
	s_add_u32 s8, s8, 0x16280
	s_addc_u32 s9, s9, 0
	global_load_dwordx4 v[188:191], v76, s[8:9]
	s_add_u32 s8, s8, 0x16280
	s_addc_u32 s9, s9, 0
	global_load_dwordx4 v[192:195], v76, s[8:9]
	s_add_u32 s8, s8, 0x16280
	s_addc_u32 s9, s9, 0
	global_load_dwordx4 v[196:199], v76, s[8:9]
	s_add_u32 s8, s8, 0x16280
	s_addc_u32 s9, s9, 0
	global_load_dwordx4 v[200:203], v76, s[8:9]
	s_add_u32 s8, s8, 0x16280
	s_addc_u32 s9, s9, 0
	global_load_dwordx4 v[204:207], v76, s[8:9]
	s_add_i32 s24, s23, 40
	s_mul_i32 s20, s24, 0x100000
	s_add_u32 s6, s48, s20
	s_addc_u32 s7, s49, 0
	s_cmp_lt_u32 s24, 16
	s_cselect_b32 s20, 1, 0
	s_sub_i32 s21, s24, 16
	s_bitcmp0_b32 s21, 2
	s_cselect_b32 s21, 1, 0
	s_cmp_lt_u32 s24, 40
	s_cselect_b32 s21, s21, 0
	s_or_b32 s20, s20, s21
	s_cmp_lg_u32 s20, 0
	s_cselect_b64 s[20:21], -1, 0
	v_cndmask_b32_e64 v91, v83, v87, s[20:21]
	v_cndmask_b32_e64 v92, v84, v88, s[20:21]
	v_cndmask_b32_e64 v93, v85, v89, s[20:21]
	v_cndmask_b32_e64 v94, v86, v90, s[20:21]
	ds_read_b32 v226, v113
	ds_read_b32 v227, v113 offset:512
	ds_read_b32 v228, v113 offset:1024
	ds_read_b32 v229, v113 offset:1536
	ds_read_b32 v230, v113 offset:2048
	ds_read_b32 v231, v113 offset:2560
	ds_read_b32 v232, v113 offset:3072
	ds_read_b32 v233, v113 offset:3584
	s_waitcnt lgkmcnt(0)
	v_bfe_u32 v120, v226, 16, 1
	v_bfe_u32 v121, v227, 16, 1
	v_bfe_u32 v122, v228, 16, 1
	v_bfe_u32 v123, v229, 16, 1
	v_bfe_u32 v124, v230, 16, 1
	v_bfe_u32 v125, v231, 16, 1
	v_bfe_u32 v126, v232, 16, 1
	v_bfe_u32 v127, v233, 16, 1
	v_add3_u32 v226, v226, v120, s63
	v_add3_u32 v227, v227, v121, s63
	v_add3_u32 v228, v228, v122, s63
	v_add3_u32 v229, v229, v123, s63
	v_add3_u32 v230, v230, v124, s63
	v_add3_u32 v231, v231, v125, s63
	v_add3_u32 v232, v232, v126, s63
	v_add3_u32 v233, v233, v127, s63
	v_perm_b32 v242, v227, v226, s64
	v_perm_b32 v243, v229, v228, s64
	v_perm_b32 v244, v231, v230, s64
	v_perm_b32 v245, v233, v232, s64
	s_nop 0
	global_store_dwordx4 v91, v[242:245], s[6:7]
	ds_read_b32 v226, v115
	ds_read_b32 v227, v115 offset:512
	ds_read_b32 v228, v115 offset:1024
	ds_read_b32 v229, v115 offset:1536
	ds_read_b32 v230, v115 offset:2048
	ds_read_b32 v231, v115 offset:2560
	ds_read_b32 v232, v115 offset:3072
	ds_read_b32 v233, v115 offset:3584
	s_waitcnt lgkmcnt(0)
	v_bfe_u32 v120, v226, 16, 1
	v_bfe_u32 v121, v227, 16, 1
	v_bfe_u32 v122, v228, 16, 1
	v_bfe_u32 v123, v229, 16, 1
	v_bfe_u32 v124, v230, 16, 1
	v_bfe_u32 v125, v231, 16, 1
	v_bfe_u32 v126, v232, 16, 1
	v_bfe_u32 v127, v233, 16, 1
	v_add3_u32 v226, v226, v120, s63
	v_add3_u32 v227, v227, v121, s63
	v_add3_u32 v228, v228, v122, s63
	v_add3_u32 v229, v229, v123, s63
	v_add3_u32 v230, v230, v124, s63
	v_add3_u32 v231, v231, v125, s63
	v_add3_u32 v232, v232, v126, s63
	v_add3_u32 v233, v233, v127, s63
	v_perm_b32 v242, v227, v226, s64
	v_perm_b32 v243, v229, v228, s64
	v_perm_b32 v244, v231, v230, s64
	v_perm_b32 v245, v233, v232, s64
	s_nop 0
	global_store_dwordx4 v92, v[242:245], s[6:7]
	ds_read_b32 v226, v117
	ds_read_b32 v227, v117 offset:512
	ds_read_b32 v228, v117 offset:1024
	ds_read_b32 v229, v117 offset:1536
	ds_read_b32 v230, v117 offset:2048
	ds_read_b32 v231, v117 offset:2560
	ds_read_b32 v232, v117 offset:3072
	ds_read_b32 v233, v117 offset:3584
	s_waitcnt lgkmcnt(0)
	v_bfe_u32 v120, v226, 16, 1
	v_bfe_u32 v121, v227, 16, 1
	v_bfe_u32 v122, v228, 16, 1
	v_bfe_u32 v123, v229, 16, 1
	v_bfe_u32 v124, v230, 16, 1
	v_bfe_u32 v125, v231, 16, 1
	v_bfe_u32 v126, v232, 16, 1
	v_bfe_u32 v127, v233, 16, 1
	v_add3_u32 v226, v226, v120, s63
	v_add3_u32 v227, v227, v121, s63
	v_add3_u32 v228, v228, v122, s63
	v_add3_u32 v229, v229, v123, s63
	v_add3_u32 v230, v230, v124, s63
	v_add3_u32 v231, v231, v125, s63
	v_add3_u32 v232, v232, v126, s63
	v_add3_u32 v233, v233, v127, s63
	v_perm_b32 v242, v227, v226, s64
	v_perm_b32 v243, v229, v228, s64
	v_perm_b32 v244, v231, v230, s64
	v_perm_b32 v245, v233, v232, s64
	s_nop 0
	global_store_dwordx4 v93, v[242:245], s[6:7]
	ds_read_b32 v226, v119
	ds_read_b32 v227, v119 offset:512
	ds_read_b32 v228, v119 offset:1024
	ds_read_b32 v229, v119 offset:1536
	ds_read_b32 v230, v119 offset:2048
	ds_read_b32 v231, v119 offset:2560
	ds_read_b32 v232, v119 offset:3072
	ds_read_b32 v233, v119 offset:3584
	s_waitcnt lgkmcnt(0)
	v_bfe_u32 v120, v226, 16, 1
	v_bfe_u32 v121, v227, 16, 1
	v_bfe_u32 v122, v228, 16, 1
	v_bfe_u32 v123, v229, 16, 1
	v_bfe_u32 v124, v230, 16, 1
	v_bfe_u32 v125, v231, 16, 1
	v_bfe_u32 v126, v232, 16, 1
	v_bfe_u32 v127, v233, 16, 1
	v_add3_u32 v226, v226, v120, s63
	v_add3_u32 v227, v227, v121, s63
	v_add3_u32 v228, v228, v122, s63
	v_add3_u32 v229, v229, v123, s63
	v_add3_u32 v230, v230, v124, s63
	v_add3_u32 v231, v231, v125, s63
	v_add3_u32 v232, v232, v126, s63
	v_add3_u32 v233, v233, v127, s63
	v_perm_b32 v242, v227, v226, s64
	v_perm_b32 v243, v229, v228, s64
	v_perm_b32 v244, v231, v230, s64
	v_perm_b32 v245, v233, v232, s64
	s_nop 0
	global_store_dwordx4 v94, v[242:245], s[6:7]
	s_waitcnt vmcnt(16)
	v_mul_f32_e32 v144, v42, v144
	v_mul_f32_e32 v145, v42, v145
	v_mul_f32_e32 v146, v42, v146
	v_mul_f32_e32 v147, v42, v147
	ds_write_b128 v209, v[144:147]
	v_mul_f32_e32 v148, v43, v148
	v_mul_f32_e32 v149, v43, v149
	v_mul_f32_e32 v150, v43, v150
	v_mul_f32_e32 v151, v43, v151
	ds_write_b128 v209, v[148:151] offset:1024
	v_mul_f32_e32 v152, v44, v152
	v_mul_f32_e32 v153, v44, v153
	v_mul_f32_e32 v154, v44, v154
	v_mul_f32_e32 v155, v44, v155
	ds_write_b128 v209, v[152:155] offset:2048
	v_mul_f32_e32 v156, v45, v156
	v_mul_f32_e32 v157, v45, v157
	v_mul_f32_e32 v158, v45, v158
	v_mul_f32_e32 v159, v45, v159
	ds_write_b128 v209, v[156:159] offset:3072
	v_mul_f32_e32 v160, v46, v160
	v_mul_f32_e32 v161, v46, v161
	v_mul_f32_e32 v162, v46, v162
	v_mul_f32_e32 v163, v46, v163
	ds_write_b128 v209, v[160:163] offset:4096
	v_mul_f32_e32 v164, v47, v164
	v_mul_f32_e32 v165, v47, v165
	v_mul_f32_e32 v166, v47, v166
	v_mul_f32_e32 v167, v47, v167
	ds_write_b128 v209, v[164:167] offset:5120
	v_mul_f32_e32 v168, v48, v168
	v_mul_f32_e32 v169, v48, v169
	v_mul_f32_e32 v170, v48, v170
	v_mul_f32_e32 v171, v48, v171
	ds_write_b128 v209, v[168:171] offset:6144
	v_mul_f32_e32 v172, v49, v172
	v_mul_f32_e32 v173, v49, v173
	v_mul_f32_e32 v174, v49, v174
	v_mul_f32_e32 v175, v49, v175
	ds_write_b128 v209, v[172:175] offset:7168
	s_waitcnt lgkmcnt(0)
	s_barrier
; #define GAS __attribute__((address_space(1)))
; #define LAS __attribute__((address_space(3)))
; #define LDS_WAIT() asm volatile("s_waitcnt lgkmcnt(0)" ::: "memory")
; __device__ __forceinline__ unsigned pk2(float lo, float hi) { return f2bf(lo) | (f2bf(hi) << 16); }
; __device__ __forceinline__ int nat_dim(int p) { return (p >> 1) + 64 * (p & 1); }
; __device__ __forceinline__ int src_col_in(int c) {
;     if (c < 5120) { const int blk = c >> 7, p = c & 127; const bool rope = blk < 16 || ((((blk - 16) >> 2) & 1) == 0); const int d = rope ? (p >> 1) + 64 * (p & 1) : p; return blk * 128 + d; }
;     if (c < OFF_Z) return c + 2096;
;     if (c < OFF_G) return c - 4048;
;     if (c < OFF_DT) return 5120 + (c - OFF_G);
;     if (c < NSRC) return c;
;     return -1;
; template <int MAP, bool KS, bool KPERM = false>
; __device__ __forceinline__ void p0_transpose_item(const float* W, int K, int Nsrc, int nblk, bf16* WT, const float* ksA, const float* ksB, int ksplit, LAS float* scr, int item, int lane) {
;     const int kb = item / nblk, nb = item % nblk, k0 = 64 * kb, n0 = 32 * nb;
;     const int nr = n0 + (lane & 31); const int sc = MAP == 1 ? src_col_in(nr) : (MAP == 2 ? nat_dim(nr) : nr);
;     float v[32];
; #pragma unroll
;     for (int i = 0; i < 32; ++i) { const int k = k0 + 2 * i + (lane >> 5); const int ksrc = KPERM ? ((k & ~127) + nat_dim(k & 127)) : k;
;         v[i] = sc >= 0 ? W[(size_t)ksrc * Nsrc + sc] : 0.f; }
; #pragma unroll
;     for (int i = 0; i < 32; ++i) { const int kk = 2 * i + (lane >> 5); const int k = k0 + kk;
;         if (KS) v[i] *= (k < ksplit ? ksA[k] : ksB[k - ksplit]);
;         scr[kk * 33 + (lane & 31)] = v[i]; }
;     LDS_WAIT(); asm volatile("" ::: "memory");
;     const int c = lane & 7;
; #pragma unroll
;     for (int j = 0; j < 4; ++j) { const int n = (lane >> 3) + 8 * j; const LAS float* s = scr + (8 * c) * 33 + n;
;         v4u o; o.x = pk2(s[0 * 33], s[1 * 33]); o.y = pk2(s[2 * 33], s[3 * 33]); o.z = pk2(s[4 * 33], s[5 * 33]); o.w = pk2(s[6 * 33], s[7 * 33]);
;         *(GAS v4u*)(WT + (size_t)(n0 + n) * K + k0 + 8 * c) = o; }
;     LDS_WAIT(); asm volatile("" ::: "memory");
	s_add_i32 s24, s23, 64
	s_lshl_b32 s20, s24, 7
	s_cmp_lt_u32 s24, 40
	s_cselect_b32 s21, 0, 0x830
	s_cmp_lt_u32 s24, 72
	s_cselect_b32 s21, s21, 0xfffff030
	s_add_i32 s20, s20, s21
	s_lshl_b32 s20, s20, 2
	s_add_u32 s8, s46, s20
	s_addc_u32 s9, s47, 0
	global_load_dwordx4 v[144:147], v76, s[8:9]
	s_add_u32 s8, s8, 0x16280
	s_addc_u32 s9, s9, 0
	global_load_dwordx4 v[148:151], v76, s[8:9]
	s_add_u32 s8, s8, 0x16280
	s_addc_u32 s9, s9, 0
	global_load_dwordx4 v[152:155], v76, s[8:9]
	s_add_u32 s8, s8, 0x16280
	s_addc_u32 s9, s9, 0
	global_load_dwordx4 v[156:159], v76, s[8:9]
	s_add_u32 s8, s8, 0x16280
	s_addc_u32 s9, s9, 0
	global_load_dwordx4 v[160:163], v76, s[8:9]
	s_add_u32 s8, s8, 0x16280
	s_addc_u32 s9, s9, 0
	global_load_dwordx4 v[164:167], v76, s[8:9]
	s_add_u32 s8, s8, 0x16280
	s_addc_u32 s9, s9, 0
	global_load_dwordx4 v[168:171], v76, s[8:9]
	s_add_u32 s8, s8, 0x16280
	s_addc_u32 s9, s9, 0
	global_load_dwordx4 v[172:175], v76, s[8:9]
	s_add_i32 s24, s23, 48
	s_mul_i32 s20, s24, 0x100000
	s_add_u32 s6, s48, s20
	s_addc_u32 s7, s49, 0
	s_cmp_lt_u32 s24, 16
	s_cselect_b32 s20, 1, 0
	s_sub_i32 s21, s24, 16
	s_bitcmp0_b32 s21, 2
	s_cselect_b32 s21, 1, 0
	s_cmp_lt_u32 s24, 40
	s_cselect_b32 s21, s21, 0
	s_or_b32 s20, s20, s21
	s_cmp_lg_u32 s20, 0
	s_cselect_b64 s[20:21], -1, 0
	v_cndmask_b32_e64 v91, v83, v87, s[20:21]
	v_cndmask_b32_e64 v92, v84, v88, s[20:21]
	v_cndmask_b32_e64 v93, v85, v89, s[20:21]
	v_cndmask_b32_e64 v94, v86, v90, s[20:21]
	ds_read_b32 v226, v112
	ds_read_b32 v227, v112 offset:512
	ds_read_b32 v228, v112 offset:1024
	ds_read_b32 v229, v112 offset:1536
	ds_read_b32 v230, v112 offset:2048
	ds_read_b32 v231, v112 offset:2560
	ds_read_b32 v232, v112 offset:3072
	ds_read_b32 v233, v112 offset:3584
	s_waitcnt lgkmcnt(0)
	v_bfe_u32 v120, v226, 16, 1
	v_bfe_u32 v121, v227, 16, 1
	v_bfe_u32 v122, v228, 16, 1
	v_bfe_u32 v123, v229, 16, 1
	v_bfe_u32 v124, v230, 16, 1
	v_bfe_u32 v125, v231, 16, 1
	v_bfe_u32 v126, v232, 16, 1
	v_bfe_u32 v127, v233, 16, 1
	v_add3_u32 v226, v226, v120, s63
	v_add3_u32 v227, v227, v121, s63
	v_add3_u32 v228, v228, v122, s63
	v_add3_u32 v229, v229, v123, s63
	v_add3_u32 v230, v230, v124, s63
	v_add3_u32 v231, v231, v125, s63
	v_add3_u32 v232, v232, v126, s63
	v_add3_u32 v233, v233, v127, s63
	v_perm_b32 v242, v227, v226, s64
	v_perm_b32 v243, v229, v228, s64
	v_perm_b32 v244, v231, v230, s64
	v_perm_b32 v245, v233, v232, s64
	s_nop 0
	global_store_dwordx4 v91, v[242:245], s[6:7]
	ds_read_b32 v226, v114
	ds_read_b32 v227, v114 offset:512
	ds_read_b32 v228, v114 offset:1024
	ds_read_b32 v229, v114 offset:1536
	ds_read_b32 v230, v114 offset:2048
	ds_read_b32 v231, v114 offset:2560
	ds_read_b32 v232, v114 offset:3072
	ds_read_b32 v233, v114 offset:3584
	s_waitcnt lgkmcnt(0)
	v_bfe_u32 v120, v226, 16, 1
	v_bfe_u32 v121, v227, 16, 1
	v_bfe_u32 v122, v228, 16, 1
	v_bfe_u32 v123, v229, 16, 1
	v_bfe_u32 v124, v230, 16, 1
	v_bfe_u32 v125, v231, 16, 1
	v_bfe_u32 v126, v232, 16, 1
	v_bfe_u32 v127, v233, 16, 1
	v_add3_u32 v226, v226, v120, s63
	v_add3_u32 v227, v227, v121, s63
	v_add3_u32 v228, v228, v122, s63
	v_add3_u32 v229, v229, v123, s63
	v_add3_u32 v230, v230, v124, s63
	v_add3_u32 v231, v231, v125, s63
	v_add3_u32 v232, v232, v126, s63
	v_add3_u32 v233, v233, v127, s63
	v_perm_b32 v242, v227, v226, s64
	v_perm_b32 v243, v229, v228, s64
	v_perm_b32 v244, v231, v230, s64
	v_perm_b32 v245, v233, v232, s64
	s_nop 0
	global_store_dwordx4 v92, v[242:245], s[6:7]
	ds_read_b32 v226, v116
	ds_read_b32 v227, v116 offset:512
	ds_read_b32 v228, v116 offset:1024
	ds_read_b32 v229, v116 offset:1536
	ds_read_b32 v230, v116 offset:2048
	ds_read_b32 v231, v116 offset:2560
	ds_read_b32 v232, v116 offset:3072
	ds_read_b32 v233, v116 offset:3584
	s_waitcnt lgkmcnt(0)
	v_bfe_u32 v120, v226, 16, 1
	v_bfe_u32 v121, v227, 16, 1
	v_bfe_u32 v122, v228, 16, 1
	v_bfe_u32 v123, v229, 16, 1
	v_bfe_u32 v124, v230, 16, 1
	v_bfe_u32 v125, v231, 16, 1
	v_bfe_u32 v126, v232, 16, 1
	v_bfe_u32 v127, v233, 16, 1
	v_add3_u32 v226, v226, v120, s63
	v_add3_u32 v227, v227, v121, s63
	v_add3_u32 v228, v228, v122, s63
	v_add3_u32 v229, v229, v123, s63
	v_add3_u32 v230, v230, v124, s63
	v_add3_u32 v231, v231, v125, s63
	v_add3_u32 v232, v232, v126, s63
	v_add3_u32 v233, v233, v127, s63
	v_perm_b32 v242, v227, v226, s64
	v_perm_b32 v243, v229, v228, s64
	v_perm_b32 v244, v231, v230, s64
	v_perm_b32 v245, v233, v232, s64
	s_nop 0
	global_store_dwordx4 v93, v[242:245], s[6:7]
	ds_read_b32 v226, v118
	ds_read_b32 v227, v118 offset:512
	ds_read_b32 v228, v118 offset:1024
	ds_read_b32 v229, v118 offset:1536
	ds_read_b32 v230, v118 offset:2048
	ds_read_b32 v231, v118 offset:2560
	ds_read_b32 v232, v118 offset:3072
	ds_read_b32 v233, v118 offset:3584
	s_waitcnt lgkmcnt(0)
	v_bfe_u32 v120, v226, 16, 1
	v_bfe_u32 v121, v227, 16, 1
	v_bfe_u32 v122, v228, 16, 1
	v_bfe_u32 v123, v229, 16, 1
	v_bfe_u32 v124, v230, 16, 1
	v_bfe_u32 v125, v231, 16, 1
	v_bfe_u32 v126, v232, 16, 1
	v_bfe_u32 v127, v233, 16, 1
	v_add3_u32 v226, v226, v120, s63
	v_add3_u32 v227, v227, v121, s63
	v_add3_u32 v228, v228, v122, s63
	v_add3_u32 v229, v229, v123, s63
	v_add3_u32 v230, v230, v124, s63
	v_add3_u32 v231, v231, v125, s63
	v_add3_u32 v232, v232, v126, s63
	v_add3_u32 v233, v233, v127, s63
	v_perm_b32 v242, v227, v226, s64
	v_perm_b32 v243, v229, v228, s64
	v_perm_b32 v244, v231, v230, s64
	v_perm_b32 v245, v233, v232, s64
	s_nop 0
	global_store_dwordx4 v94, v[242:245], s[6:7]
	s_waitcnt vmcnt(16)
	v_mul_f32_e32 v176, v42, v176
	v_mul_f32_e32 v177, v42, v177
	v_mul_f32_e32 v178, v42, v178
	v_mul_f32_e32 v179, v42, v179
	ds_write_b128 v210, v[176:179]
	v_mul_f32_e32 v180, v43, v180
	v_mul_f32_e32 v181, v43, v181
	v_mul_f32_e32 v182, v43, v182
	v_mul_f32_e32 v183, v43, v183
	ds_write_b128 v210, v[180:183] offset:1024
	v_mul_f32_e32 v184, v44, v184
	v_mul_f32_e32 v185, v44, v185
	v_mul_f32_e32 v186, v44, v186
	v_mul_f32_e32 v187, v44, v187
	ds_write_b128 v210, v[184:187] offset:2048
	v_mul_f32_e32 v188, v45, v188
	v_mul_f32_e32 v189, v45, v189
	v_mul_f32_e32 v190, v45, v190
	v_mul_f32_e32 v191, v45, v191
	ds_write_b128 v210, v[188:191] offset:3072
	v_mul_f32_e32 v192, v46, v192
	v_mul_f32_e32 v193, v46, v193
	v_mul_f32_e32 v194, v46, v194
	v_mul_f32_e32 v195, v46, v195
	ds_write_b128 v210, v[192:195] offset:4096
	v_mul_f32_e32 v196, v47, v196
	v_mul_f32_e32 v197, v47, v197
	v_mul_f32_e32 v198, v47, v198
	v_mul_f32_e32 v199, v47, v199
	ds_write_b128 v210, v[196:199] offset:5120
	v_mul_f32_e32 v200, v48, v200
	v_mul_f32_e32 v201, v48, v201
	v_mul_f32_e32 v202, v48, v202
	v_mul_f32_e32 v203, v48, v203
	ds_write_b128 v210, v[200:203] offset:6144
	v_mul_f32_e32 v204, v49, v204
	v_mul_f32_e32 v205, v49, v205
	v_mul_f32_e32 v206, v49, v206
	v_mul_f32_e32 v207, v49, v207
	ds_write_b128 v210, v[204:207] offset:7168
	s_waitcnt lgkmcnt(0)
	s_barrier
; #define GAS __attribute__((address_space(1)))
; #define LAS __attribute__((address_space(3)))
; #define LDS_WAIT() asm volatile("s_waitcnt lgkmcnt(0)" ::: "memory")
; __device__ __forceinline__ unsigned pk2(float lo, float hi) { return f2bf(lo) | (f2bf(hi) << 16); }
; __device__ __forceinline__ int nat_dim(int p) { return (p >> 1) + 64 * (p & 1); }
; __device__ __forceinline__ int src_col_in(int c) {
;     if (c < 5120) { const int blk = c >> 7, p = c & 127; const bool rope = blk < 16 || ((((blk - 16) >> 2) & 1) == 0); const int d = rope ? (p >> 1) + 64 * (p & 1) : p; return blk * 128 + d; }
;     if (c < OFF_Z) return c + 2096;
;     if (c < OFF_G) return c - 4048;
;     if (c < OFF_DT) return 5120 + (c - OFF_G);
;     if (c < NSRC) return c;
;     return -1;
; template <int MAP, bool KS, bool KPERM = false>
; __device__ __forceinline__ void p0_transpose_item(const float* W, int K, int Nsrc, int nblk, bf16* WT, const float* ksA, const float* ksB, int ksplit, LAS float* scr, int item, int lane) {
;     const int kb = item / nblk, nb = item % nblk, k0 = 64 * kb, n0 = 32 * nb;
;     const int nr = n0 + (lane & 31); const int sc = MAP == 1 ? src_col_in(nr) : (MAP == 2 ? nat_dim(nr) : nr);
;     float v[32];
; #pragma unroll
;     for (int i = 0; i < 32; ++i) { const int k = k0 + 2 * i + (lane >> 5); const int ksrc = KPERM ? ((k & ~127) + nat_dim(k & 127)) : k;
;         v[i] = sc >= 0 ? W[(size_t)ksrc * Nsrc + sc] : 0.f; }
; #pragma unroll
;     for (int i = 0; i < 32; ++i) { const int kk = 2 * i + (lane >> 5); const int k = k0 + kk;
;         if (KS) v[i] *= (k < ksplit ? ksA[k] : ksB[k - ksplit]);
;         scr[kk * 33 + (lane & 31)] = v[i]; }
;     LDS_WAIT(); asm volatile("" ::: "memory");
;     const int c = lane & 7;
; #pragma unroll
;     for (int j = 0; j < 4; ++j) { const int n = (lane >> 3) + 8 * j; const LAS float* s = scr + (8 * c) * 33 + n;
;         v4u o; o.x = pk2(s[0 * 33], s[1 * 33]); o.y = pk2(s[2 * 33], s[3 * 33]); o.z = pk2(s[4 * 33], s[5 * 33]); o.w = pk2(s[6 * 33], s[7 * 33]);
;         *(GAS v4u*)(WT + (size_t)(n0 + n) * K + k0 + 8 * c) = o; }
;     LDS_WAIT(); asm volatile("" ::: "memory");
	s_add_i32 s24, s23, 72
	s_lshl_b32 s20, s24, 7
	s_cmp_lt_u32 s24, 40
	s_cselect_b32 s21, 0, 0x830
	s_cmp_lt_u32 s24, 72
	s_cselect_b32 s21, s21, 0xfffff030
	s_add_i32 s20, s20, s21
	s_lshl_b32 s20, s20, 2
	s_add_u32 s8, s46, s20
	s_addc_u32 s9, s47, 0
	global_load_dwordx4 v[176:179], v76, s[8:9]
	s_add_u32 s8, s8, 0x16280
	s_addc_u32 s9, s9, 0
	global_load_dwordx4 v[180:183], v76, s[8:9]
	s_add_u32 s8, s8, 0x16280
	s_addc_u32 s9, s9, 0
	global_load_dwordx4 v[184:187], v76, s[8:9]
	s_add_u32 s8, s8, 0x16280
	s_addc_u32 s9, s9, 0
	global_load_dwordx4 v[188:191], v76, s[8:9]
	s_add_u32 s8, s8, 0x16280
	s_addc_u32 s9, s9, 0
	global_load_dwordx4 v[192:195], v76, s[8:9]
	s_add_u32 s8, s8, 0x16280
	s_addc_u32 s9, s9, 0
	global_load_dwordx4 v[196:199], v76, s[8:9]
	s_add_u32 s8, s8, 0x16280
	s_addc_u32 s9, s9, 0
	global_load_dwordx4 v[200:203], v76, s[8:9]
	s_add_u32 s8, s8, 0x16280
	s_addc_u32 s9, s9, 0
	global_load_dwordx4 v[204:207], v76, s[8:9]
	s_add_i32 s24, s23, 56
	s_mul_i32 s20, s24, 0x100000
	s_add_u32 s6, s48, s20
	s_addc_u32 s7, s49, 0
	s_cmp_lt_u32 s24, 16
	s_cselect_b32 s20, 1, 0
	s_sub_i32 s21, s24, 16
	s_bitcmp0_b32 s21, 2
	s_cselect_b32 s21, 1, 0
	s_cmp_lt_u32 s24, 40
	s_cselect_b32 s21, s21, 0
	s_or_b32 s20, s20, s21
	s_cmp_lg_u32 s20, 0
	s_cselect_b64 s[20:21], -1, 0
	v_cndmask_b32_e64 v91, v83, v87, s[20:21]
	v_cndmask_b32_e64 v92, v84, v88, s[20:21]
	v_cndmask_b32_e64 v93, v85, v89, s[20:21]
	v_cndmask_b32_e64 v94, v86, v90, s[20:21]
	ds_read_b32 v226, v113
	ds_read_b32 v227, v113 offset:512
	ds_read_b32 v228, v113 offset:1024
	ds_read_b32 v229, v113 offset:1536
	ds_read_b32 v230, v113 offset:2048
	ds_read_b32 v231, v113 offset:2560
	ds_read_b32 v232, v113 offset:3072
	ds_read_b32 v233, v113 offset:3584
	s_waitcnt lgkmcnt(0)
	v_bfe_u32 v120, v226, 16, 1
	v_bfe_u32 v121, v227, 16, 1
	v_bfe_u32 v122, v228, 16, 1
	v_bfe_u32 v123, v229, 16, 1
	v_bfe_u32 v124, v230, 16, 1
	v_bfe_u32 v125, v231, 16, 1
	v_bfe_u32 v126, v232, 16, 1
	v_bfe_u32 v127, v233, 16, 1
	v_add3_u32 v226, v226, v120, s63
	v_add3_u32 v227, v227, v121, s63
	v_add3_u32 v228, v228, v122, s63
	v_add3_u32 v229, v229, v123, s63
	v_add3_u32 v230, v230, v124, s63
	v_add3_u32 v231, v231, v125, s63
	v_add3_u32 v232, v232, v126, s63
	v_add3_u32 v233, v233, v127, s63
	v_perm_b32 v242, v227, v226, s64
	v_perm_b32 v243, v229, v228, s64
	v_perm_b32 v244, v231, v230, s64
	v_perm_b32 v245, v233, v232, s64
	s_nop 0
	global_store_dwordx4 v91, v[242:245], s[6:7]
	ds_read_b32 v226, v115
	ds_read_b32 v227, v115 offset:512
	ds_read_b32 v228, v115 offset:1024
	ds_read_b32 v229, v115 offset:1536
	ds_read_b32 v230, v115 offset:2048
	ds_read_b32 v231, v115 offset:2560
	ds_read_b32 v232, v115 offset:3072
	ds_read_b32 v233, v115 offset:3584
	s_waitcnt lgkmcnt(0)
	v_bfe_u32 v120, v226, 16, 1
	v_bfe_u32 v121, v227, 16, 1
	v_bfe_u32 v122, v228, 16, 1
	v_bfe_u32 v123, v229, 16, 1
	v_bfe_u32 v124, v230, 16, 1
	v_bfe_u32 v125, v231, 16, 1
	v_bfe_u32 v126, v232, 16, 1
	v_bfe_u32 v127, v233, 16, 1
	v_add3_u32 v226, v226, v120, s63
	v_add3_u32 v227, v227, v121, s63
	v_add3_u32 v228, v228, v122, s63
	v_add3_u32 v229, v229, v123, s63
	v_add3_u32 v230, v230, v124, s63
	v_add3_u32 v231, v231, v125, s63
	v_add3_u32 v232, v232, v126, s63
	v_add3_u32 v233, v233, v127, s63
	v_perm_b32 v242, v227, v226, s64
	v_perm_b32 v243, v229, v228, s64
	v_perm_b32 v244, v231, v230, s64
	v_perm_b32 v245, v233, v232, s64
	s_nop 0
	global_store_dwordx4 v92, v[242:245], s[6:7]
	ds_read_b32 v226, v117
	ds_read_b32 v227, v117 offset:512
	ds_read_b32 v228, v117 offset:1024
	ds_read_b32 v229, v117 offset:1536
	ds_read_b32 v230, v117 offset:2048
	ds_read_b32 v231, v117 offset:2560
	ds_read_b32 v232, v117 offset:3072
	ds_read_b32 v233, v117 offset:3584
	s_waitcnt lgkmcnt(0)
	v_bfe_u32 v120, v226, 16, 1
	v_bfe_u32 v121, v227, 16, 1
	v_bfe_u32 v122, v228, 16, 1
	v_bfe_u32 v123, v229, 16, 1
	v_bfe_u32 v124, v230, 16, 1
	v_bfe_u32 v125, v231, 16, 1
	v_bfe_u32 v126, v232, 16, 1
	v_bfe_u32 v127, v233, 16, 1
	v_add3_u32 v226, v226, v120, s63
	v_add3_u32 v227, v227, v121, s63
	v_add3_u32 v228, v228, v122, s63
	v_add3_u32 v229, v229, v123, s63
	v_add3_u32 v230, v230, v124, s63
	v_add3_u32 v231, v231, v125, s63
	v_add3_u32 v232, v232, v126, s63
	v_add3_u32 v233, v233, v127, s63
	v_perm_b32 v242, v227, v226, s64
	v_perm_b32 v243, v229, v228, s64
	v_perm_b32 v244, v231, v230, s64
	v_perm_b32 v245, v233, v232, s64
	s_nop 0
	global_store_dwordx4 v93, v[242:245], s[6:7]
	ds_read_b32 v226, v119
	ds_read_b32 v227, v119 offset:512
	ds_read_b32 v228, v119 offset:1024
	ds_read_b32 v229, v119 offset:1536
	ds_read_b32 v230, v119 offset:2048
	ds_read_b32 v231, v119 offset:2560
	ds_read_b32 v232, v119 offset:3072
	ds_read_b32 v233, v119 offset:3584
	s_waitcnt lgkmcnt(0)
	v_bfe_u32 v120, v226, 16, 1
	v_bfe_u32 v121, v227, 16, 1
	v_bfe_u32 v122, v228, 16, 1
	v_bfe_u32 v123, v229, 16, 1
	v_bfe_u32 v124, v230, 16, 1
	v_bfe_u32 v125, v231, 16, 1
	v_bfe_u32 v126, v232, 16, 1
	v_bfe_u32 v127, v233, 16, 1
	v_add3_u32 v226, v226, v120, s63
	v_add3_u32 v227, v227, v121, s63
	v_add3_u32 v228, v228, v122, s63
	v_add3_u32 v229, v229, v123, s63
	v_add3_u32 v230, v230, v124, s63
	v_add3_u32 v231, v231, v125, s63
	v_add3_u32 v232, v232, v126, s63
	v_add3_u32 v233, v233, v127, s63
	v_perm_b32 v242, v227, v226, s64
	v_perm_b32 v243, v229, v228, s64
	v_perm_b32 v244, v231, v230, s64
	v_perm_b32 v245, v233, v232, s64
	s_nop 0
	global_store_dwordx4 v94, v[242:245], s[6:7]
	s_waitcnt vmcnt(16)
	v_mul_f32_e32 v144, v42, v144
	v_mul_f32_e32 v145, v42, v145
	v_mul_f32_e32 v146, v42, v146
	v_mul_f32_e32 v147, v42, v147
	ds_write_b128 v209, v[144:147]
	v_mul_f32_e32 v148, v43, v148
	v_mul_f32_e32 v149, v43, v149
	v_mul_f32_e32 v150, v43, v150
	v_mul_f32_e32 v151, v43, v151
	ds_write_b128 v209, v[148:151] offset:1024
	v_mul_f32_e32 v152, v44, v152
	v_mul_f32_e32 v153, v44, v153
	v_mul_f32_e32 v154, v44, v154
	v_mul_f32_e32 v155, v44, v155
	ds_write_b128 v209, v[152:155] offset:2048
	v_mul_f32_e32 v156, v45, v156
	v_mul_f32_e32 v157, v45, v157
	v_mul_f32_e32 v158, v45, v158
	v_mul_f32_e32 v159, v45, v159
	ds_write_b128 v209, v[156:159] offset:3072
	v_mul_f32_e32 v160, v46, v160
	v_mul_f32_e32 v161, v46, v161
	v_mul_f32_e32 v162, v46, v162
	v_mul_f32_e32 v163, v46, v163
	ds_write_b128 v209, v[160:163] offset:4096
	v_mul_f32_e32 v164, v47, v164
	v_mul_f32_e32 v165, v47, v165
	v_mul_f32_e32 v166, v47, v166
	v_mul_f32_e32 v167, v47, v167
	ds_write_b128 v209, v[164:167] offset:5120
	v_mul_f32_e32 v168, v48, v168
	v_mul_f32_e32 v169, v48, v169
	v_mul_f32_e32 v170, v48, v170
	v_mul_f32_e32 v171, v48, v171
	ds_write_b128 v209, v[168:171] offset:6144
	v_mul_f32_e32 v172, v49, v172
	v_mul_f32_e32 v173, v49, v173
	v_mul_f32_e32 v174, v49, v174
	v_mul_f32_e32 v175, v49, v175
	ds_write_b128 v209, v[172:175] offset:7168
	s_waitcnt lgkmcnt(0)
	s_barrier
; #define GAS __attribute__((address_space(1)))
; #define LAS __attribute__((address_space(3)))
; #define LDS_WAIT() asm volatile("s_waitcnt lgkmcnt(0)" ::: "memory")
; __device__ __forceinline__ unsigned pk2(float lo, float hi) { return f2bf(lo) | (f2bf(hi) << 16); }
; __device__ __forceinline__ int nat_dim(int p) { return (p >> 1) + 64 * (p & 1); }
; __device__ __forceinline__ int src_col_in(int c) {
;     if (c < 5120) { const int blk = c >> 7, p = c & 127; const bool rope = blk < 16 || ((((blk - 16) >> 2) & 1) == 0); const int d = rope ? (p >> 1) + 64 * (p & 1) : p; return blk * 128 + d; }
;     if (c < OFF_Z) return c + 2096;
;     if (c < OFF_G) return c - 4048;
;     if (c < OFF_DT) return 5120 + (c - OFF_G);
;     if (c < NSRC) return c;
;     return -1;
; template <int MAP, bool KS, bool KPERM = false>
; __device__ __forceinline__ void p0_transpose_item(const float* W, int K, int Nsrc, int nblk, bf16* WT, const float* ksA, const float* ksB, int ksplit, LAS float* scr, int item, int lane) {
;     const int kb = item / nblk, nb = item % nblk, k0 = 64 * kb, n0 = 32 * nb;
;     const int nr = n0 + (lane & 31); const int sc = MAP == 1 ? src_col_in(nr) : (MAP == 2 ? nat_dim(nr) : nr);
;     float v[32];
; #pragma unroll
;     for (int i = 0; i < 32; ++i) { const int k = k0 + 2 * i + (lane >> 5); const int ksrc = KPERM ? ((k & ~127) + nat_dim(k & 127)) : k;
;         v[i] = sc >= 0 ? W[(size_t)ksrc * Nsrc + sc] : 0.f; }
; #pragma unroll
;     for (int i = 0; i < 32; ++i) { const int kk = 2 * i + (lane >> 5); const int k = k0 + kk;
;         if (KS) v[i] *= (k < ksplit ? ksA[k] : ksB[k - ksplit]);
;         scr[kk * 33 + (lane & 31)] = v[i]; }
;     LDS_WAIT(); asm volatile("" ::: "memory");
;     const int c = lane & 7;
; #pragma unroll
;     for (int j = 0; j < 4; ++j) { const int n = (lane >> 3) + 8 * j; const LAS float* s = scr + (8 * c) * 33 + n;
;         v4u o; o.x = pk2(s[0 * 33], s[1 * 33]); o.y = pk2(s[2 * 33], s[3 * 33]); o.z = pk2(s[4 * 33], s[5 * 33]); o.w = pk2(s[6 * 33], s[7 * 33]);
;         *(GAS v4u*)(WT + (size_t)(n0 + n) * K + k0 + 8 * c) = o; }
;     LDS_WAIT(); asm volatile("" ::: "memory");
	s_add_i32 s24, s23, 80
	s_lshl_b32 s20, s24, 7
	s_cmp_lt_u32 s24, 40
	s_cselect_b32 s21, 0, 0x830
	s_cmp_lt_u32 s24, 72
	s_cselect_b32 s21, s21, 0xfffff030
	s_add_i32 s20, s20, s21
	s_lshl_b32 s20, s20, 2
	s_add_u32 s8, s46, s20
	s_addc_u32 s9, s47, 0
	global_load_dwordx4 v[144:147], v76, s[8:9]
	s_add_u32 s8, s8, 0x16280
	s_addc_u32 s9, s9, 0
	global_load_dwordx4 v[148:151], v76, s[8:9]
	s_add_u32 s8, s8, 0x16280
	s_addc_u32 s9, s9, 0
	global_load_dwordx4 v[152:155], v76, s[8:9]
	s_add_u32 s8, s8, 0x16280
	s_addc_u32 s9, s9, 0
	global_load_dwordx4 v[156:159], v76, s[8:9]
	s_add_u32 s8, s8, 0x16280
	s_addc_u32 s9, s9, 0
	global_load_dwordx4 v[160:163], v76, s[8:9]
	s_add_u32 s8, s8, 0x16280
	s_addc_u32 s9, s9, 0
	global_load_dwordx4 v[164:167], v76, s[8:9]
	s_add_u32 s8, s8, 0x16280
	s_addc_u32 s9, s9, 0
	global_load_dwordx4 v[168:171], v76, s[8:9]
	s_add_u32 s8, s8, 0x16280
	s_addc_u32 s9, s9, 0
	global_load_dwordx4 v[172:175], v76, s[8:9]
	s_add_i32 s24, s23, 64
	s_mul_i32 s20, s24, 0x100000
	s_add_u32 s6, s48, s20
	s_addc_u32 s7, s49, 0
	s_cmp_lt_u32 s24, 16
	s_cselect_b32 s20, 1, 0
	s_sub_i32 s21, s24, 16
	s_bitcmp0_b32 s21, 2
	s_cselect_b32 s21, 1, 0
	s_cmp_lt_u32 s24, 40
	s_cselect_b32 s21, s21, 0
	s_or_b32 s20, s20, s21
	s_cmp_lg_u32 s20, 0
	s_cselect_b64 s[20:21], -1, 0
	v_cndmask_b32_e64 v91, v83, v87, s[20:21]
	v_cndmask_b32_e64 v92, v84, v88, s[20:21]
	v_cndmask_b32_e64 v93, v85, v89, s[20:21]
	v_cndmask_b32_e64 v94, v86, v90, s[20:21]
	ds_read_b32 v226, v112
	ds_read_b32 v227, v112 offset:512
	ds_read_b32 v228, v112 offset:1024
	ds_read_b32 v229, v112 offset:1536
	ds_read_b32 v230, v112 offset:2048
	ds_read_b32 v231, v112 offset:2560
	ds_read_b32 v232, v112 offset:3072
	ds_read_b32 v233, v112 offset:3584
	s_waitcnt lgkmcnt(0)
	v_bfe_u32 v120, v226, 16, 1
	v_bfe_u32 v121, v227, 16, 1
	v_bfe_u32 v122, v228, 16, 1
	v_bfe_u32 v123, v229, 16, 1
	v_bfe_u32 v124, v230, 16, 1
	v_bfe_u32 v125, v231, 16, 1
	v_bfe_u32 v126, v232, 16, 1
	v_bfe_u32 v127, v233, 16, 1
	v_add3_u32 v226, v226, v120, s63
	v_add3_u32 v227, v227, v121, s63
	v_add3_u32 v228, v228, v122, s63
	v_add3_u32 v229, v229, v123, s63
	v_add3_u32 v230, v230, v124, s63
	v_add3_u32 v231, v231, v125, s63
	v_add3_u32 v232, v232, v126, s63
	v_add3_u32 v233, v233, v127, s63
	v_perm_b32 v242, v227, v226, s64
	v_perm_b32 v243, v229, v228, s64
	v_perm_b32 v244, v231, v230, s64
	v_perm_b32 v245, v233, v232, s64
	s_nop 0
	global_store_dwordx4 v91, v[242:245], s[6:7]
	ds_read_b32 v226, v114
	ds_read_b32 v227, v114 offset:512
	ds_read_b32 v228, v114 offset:1024
	ds_read_b32 v229, v114 offset:1536
	ds_read_b32 v230, v114 offset:2048
	ds_read_b32 v231, v114 offset:2560
	ds_read_b32 v232, v114 offset:3072
	ds_read_b32 v233, v114 offset:3584
	s_waitcnt lgkmcnt(0)
	v_bfe_u32 v120, v226, 16, 1
	v_bfe_u32 v121, v227, 16, 1
	v_bfe_u32 v122, v228, 16, 1
	v_bfe_u32 v123, v229, 16, 1
	v_bfe_u32 v124, v230, 16, 1
	v_bfe_u32 v125, v231, 16, 1
	v_bfe_u32 v126, v232, 16, 1
	v_bfe_u32 v127, v233, 16, 1
	v_add3_u32 v226, v226, v120, s63
	v_add3_u32 v227, v227, v121, s63
	v_add3_u32 v228, v228, v122, s63
	v_add3_u32 v229, v229, v123, s63
	v_add3_u32 v230, v230, v124, s63
	v_add3_u32 v231, v231, v125, s63
	v_add3_u32 v232, v232, v126, s63
	v_add3_u32 v233, v233, v127, s63
	v_perm_b32 v242, v227, v226, s64
	v_perm_b32 v243, v229, v228, s64
	v_perm_b32 v244, v231, v230, s64
	v_perm_b32 v245, v233, v232, s64
	s_nop 0
	global_store_dwordx4 v92, v[242:245], s[6:7]
	ds_read_b32 v226, v116
	ds_read_b32 v227, v116 offset:512
	ds_read_b32 v228, v116 offset:1024
	ds_read_b32 v229, v116 offset:1536
	ds_read_b32 v230, v116 offset:2048
	ds_read_b32 v231, v116 offset:2560
	ds_read_b32 v232, v116 offset:3072
	ds_read_b32 v233, v116 offset:3584
	s_waitcnt lgkmcnt(0)
	v_bfe_u32 v120, v226, 16, 1
	v_bfe_u32 v121, v227, 16, 1
	v_bfe_u32 v122, v228, 16, 1
	v_bfe_u32 v123, v229, 16, 1
	v_bfe_u32 v124, v230, 16, 1
	v_bfe_u32 v125, v231, 16, 1
	v_bfe_u32 v126, v232, 16, 1
	v_bfe_u32 v127, v233, 16, 1
	v_add3_u32 v226, v226, v120, s63
	v_add3_u32 v227, v227, v121, s63
	v_add3_u32 v228, v228, v122, s63
	v_add3_u32 v229, v229, v123, s63
	v_add3_u32 v230, v230, v124, s63
	v_add3_u32 v231, v231, v125, s63
	v_add3_u32 v232, v232, v126, s63
	v_add3_u32 v233, v233, v127, s63
	v_perm_b32 v242, v227, v226, s64
	v_perm_b32 v243, v229, v228, s64
	v_perm_b32 v244, v231, v230, s64
	v_perm_b32 v245, v233, v232, s64
	s_nop 0
	global_store_dwordx4 v93, v[242:245], s[6:7]
	ds_read_b32 v226, v118
	ds_read_b32 v227, v118 offset:512
	ds_read_b32 v228, v118 offset:1024
	ds_read_b32 v229, v118 offset:1536
	ds_read_b32 v230, v118 offset:2048
	ds_read_b32 v231, v118 offset:2560
	ds_read_b32 v232, v118 offset:3072
	ds_read_b32 v233, v118 offset:3584
	s_waitcnt lgkmcnt(0)
	v_bfe_u32 v120, v226, 16, 1
	v_bfe_u32 v121, v227, 16, 1
	v_bfe_u32 v122, v228, 16, 1
	v_bfe_u32 v123, v229, 16, 1
	v_bfe_u32 v124, v230, 16, 1
	v_bfe_u32 v125, v231, 16, 1
	v_bfe_u32 v126, v232, 16, 1
	v_bfe_u32 v127, v233, 16, 1
	v_add3_u32 v226, v226, v120, s63
	v_add3_u32 v227, v227, v121, s63
	v_add3_u32 v228, v228, v122, s63
	v_add3_u32 v229, v229, v123, s63
	v_add3_u32 v230, v230, v124, s63
	v_add3_u32 v231, v231, v125, s63
	v_add3_u32 v232, v232, v126, s63
	v_add3_u32 v233, v233, v127, s63
	v_perm_b32 v242, v227, v226, s64
	v_perm_b32 v243, v229, v228, s64
	v_perm_b32 v244, v231, v230, s64
	v_perm_b32 v245, v233, v232, s64
	s_nop 0
	global_store_dwordx4 v94, v[242:245], s[6:7]
	s_waitcnt vmcnt(16)
	v_mul_f32_e32 v176, v42, v176
	v_mul_f32_e32 v177, v42, v177
	v_mul_f32_e32 v178, v42, v178
	v_mul_f32_e32 v179, v42, v179
	ds_write_b128 v210, v[176:179]
	v_mul_f32_e32 v180, v43, v180
	v_mul_f32_e32 v181, v43, v181
	v_mul_f32_e32 v182, v43, v182
	v_mul_f32_e32 v183, v43, v183
	ds_write_b128 v210, v[180:183] offset:1024
	v_mul_f32_e32 v184, v44, v184
	v_mul_f32_e32 v185, v44, v185
	v_mul_f32_e32 v186, v44, v186
	v_mul_f32_e32 v187, v44, v187
	ds_write_b128 v210, v[184:187] offset:2048
	v_mul_f32_e32 v188, v45, v188
	v_mul_f32_e32 v189, v45, v189
	v_mul_f32_e32 v190, v45, v190
	v_mul_f32_e32 v191, v45, v191
	ds_write_b128 v210, v[188:191] offset:3072
	v_mul_f32_e32 v192, v46, v192
	v_mul_f32_e32 v193, v46, v193
	v_mul_f32_e32 v194, v46, v194
	v_mul_f32_e32 v195, v46, v195
	ds_write_b128 v210, v[192:195] offset:4096
	v_mul_f32_e32 v196, v47, v196
	v_mul_f32_e32 v197, v47, v197
	v_mul_f32_e32 v198, v47, v198
	v_mul_f32_e32 v199, v47, v199
	ds_write_b128 v210, v[196:199] offset:5120
	v_mul_f32_e32 v200, v48, v200
	v_mul_f32_e32 v201, v48, v201
	v_mul_f32_e32 v202, v48, v202
	v_mul_f32_e32 v203, v48, v203
	ds_write_b128 v210, v[200:203] offset:6144
	v_mul_f32_e32 v204, v49, v204
	v_mul_f32_e32 v205, v49, v205
	v_mul_f32_e32 v206, v49, v206
	v_mul_f32_e32 v207, v49, v207
	ds_write_b128 v210, v[204:207] offset:7168
	s_waitcnt lgkmcnt(0)
	s_barrier
; #define GAS __attribute__((address_space(1)))
; #define LAS __attribute__((address_space(3)))
; #define LDS_WAIT() asm volatile("s_waitcnt lgkmcnt(0)" ::: "memory")
; __device__ __forceinline__ unsigned pk2(float lo, float hi) { return f2bf(lo) | (f2bf(hi) << 16); }
; __device__ __forceinline__ int nat_dim(int p) { return (p >> 1) + 64 * (p & 1); }
; __device__ __forceinline__ int src_col_in(int c) {
;     if (c < 5120) { const int blk = c >> 7, p = c & 127; const bool rope = blk < 16 || ((((blk - 16) >> 2) & 1) == 0); const int d = rope ? (p >> 1) + 64 * (p & 1) : p; return blk * 128 + d; }
;     if (c < OFF_Z) return c + 2096;
;     if (c < OFF_G) return c - 4048;
;     if (c < OFF_DT) return 5120 + (c - OFF_G);
;     if (c < NSRC) return c;
;     return -1;
; template <int MAP, bool KS, bool KPERM = false>
; __device__ __forceinline__ void p0_transpose_item(const float* W, int K, int Nsrc, int nblk, bf16* WT, const float* ksA, const float* ksB, int ksplit, LAS float* scr, int item, int lane) {
;     const int kb = item / nblk, nb = item % nblk, k0 = 64 * kb, n0 = 32 * nb;
;     const int nr = n0 + (lane & 31); const int sc = MAP == 1 ? src_col_in(nr) : (MAP == 2 ? nat_dim(nr) : nr);
;     float v[32];
; #pragma unroll
;     for (int i = 0; i < 32; ++i) { const int k = k0 + 2 * i + (lane >> 5); const int ksrc = KPERM ? ((k & ~127) + nat_dim(k & 127)) : k;
;         v[i] = sc >= 0 ? W[(size_t)ksrc * Nsrc + sc] : 0.f; }
; #pragma unroll
;     for (int i = 0; i < 32; ++i) { const int kk = 2 * i + (lane >> 5); const int k = k0 + kk;
;         if (KS) v[i] *= (k < ksplit ? ksA[k] : ksB[k - ksplit]);
;         scr[kk * 33 + (lane & 31)] = v[i]; }
;     LDS_WAIT(); asm volatile("" ::: "memory");
;     const int c = lane & 7;
; #pragma unroll
;     for (int j = 0; j < 4; ++j) { const int n = (lane >> 3) + 8 * j; const LAS float* s = scr + (8 * c) * 33 + n;
;         v4u o; o.x = pk2(s[0 * 33], s[1 * 33]); o.y = pk2(s[2 * 33], s[3 * 33]); o.z = pk2(s[4 * 33], s[5 * 33]); o.w = pk2(s[6 * 33], s[7 * 33]);
;         *(GAS v4u*)(WT + (size_t)(n0 + n) * K + k0 + 8 * c) = o; }
;     LDS_WAIT(); asm volatile("" ::: "memory");
	s_add_i32 s24, s23, 0
	s_lshl_b32 s20, s24, 7
	s_cmp_lt_u32 s24, 40
	s_cselect_b32 s21, 0, 0x830
	s_cmp_lt_u32 s24, 72
	s_cselect_b32 s21, s21, 0xfffff030
	s_add_i32 s20, s20, s21
	s_lshl_b32 s20, s20, 2
	s_add_u32 s8, s50, s20
	s_addc_u32 s9, s51, 0
	global_load_dwordx4 v[176:179], v76, s[8:9]
	s_add_u32 s8, s8, 0x16280
	s_addc_u32 s9, s9, 0
	global_load_dwordx4 v[180:183], v76, s[8:9]
	s_add_u32 s8, s8, 0x16280
	s_addc_u32 s9, s9, 0
	global_load_dwordx4 v[184:187], v76, s[8:9]
	s_add_u32 s8, s8, 0x16280
	s_addc_u32 s9, s9, 0
	global_load_dwordx4 v[188:191], v76, s[8:9]
	s_add_u32 s8, s8, 0x16280
	s_addc_u32 s9, s9, 0
	global_load_dwordx4 v[192:195], v76, s[8:9]
	s_add_u32 s8, s8, 0x16280
	s_addc_u32 s9, s9, 0
	global_load_dwordx4 v[196:199], v76, s[8:9]
	s_add_u32 s8, s8, 0x16280
	s_addc_u32 s9, s9, 0
	global_load_dwordx4 v[200:203], v76, s[8:9]
	s_add_u32 s8, s8, 0x16280
	s_addc_u32 s9, s9, 0
	global_load_dwordx4 v[204:207], v76, s[8:9]
	s_add_i32 s24, s23, 72
	s_mul_i32 s20, s24, 0x100000
	s_add_u32 s6, s48, s20
	s_addc_u32 s7, s49, 0
	s_cmp_lt_u32 s24, 16
	s_cselect_b32 s20, 1, 0
	s_sub_i32 s21, s24, 16
	s_bitcmp0_b32 s21, 2
	s_cselect_b32 s21, 1, 0
	s_cmp_lt_u32 s24, 40
	s_cselect_b32 s21, s21, 0
	s_or_b32 s20, s20, s21
	s_cmp_lg_u32 s20, 0
	s_cselect_b64 s[20:21], -1, 0
	v_cndmask_b32_e64 v91, v83, v87, s[20:21]
	v_cndmask_b32_e64 v92, v84, v88, s[20:21]
	v_cndmask_b32_e64 v93, v85, v89, s[20:21]
	v_cndmask_b32_e64 v94, v86, v90, s[20:21]
	ds_read_b32 v226, v113
	ds_read_b32 v227, v113 offset:512
	ds_read_b32 v228, v113 offset:1024
	ds_read_b32 v229, v113 offset:1536
	ds_read_b32 v230, v113 offset:2048
	ds_read_b32 v231, v113 offset:2560
	ds_read_b32 v232, v113 offset:3072
	ds_read_b32 v233, v113 offset:3584
	s_waitcnt lgkmcnt(0)
	v_bfe_u32 v120, v226, 16, 1
	v_bfe_u32 v121, v227, 16, 1
	v_bfe_u32 v122, v228, 16, 1
	v_bfe_u32 v123, v229, 16, 1
	v_bfe_u32 v124, v230, 16, 1
	v_bfe_u32 v125, v231, 16, 1
	v_bfe_u32 v126, v232, 16, 1
	v_bfe_u32 v127, v233, 16, 1
	v_add3_u32 v226, v226, v120, s63
	v_add3_u32 v227, v227, v121, s63
	v_add3_u32 v228, v228, v122, s63
	v_add3_u32 v229, v229, v123, s63
	v_add3_u32 v230, v230, v124, s63
	v_add3_u32 v231, v231, v125, s63
	v_add3_u32 v232, v232, v126, s63
	v_add3_u32 v233, v233, v127, s63
	v_perm_b32 v242, v227, v226, s64
	v_perm_b32 v243, v229, v228, s64
	v_perm_b32 v244, v231, v230, s64
	v_perm_b32 v245, v233, v232, s64
	s_nop 0
	global_store_dwordx4 v91, v[242:245], s[6:7]
	ds_read_b32 v226, v115
	ds_read_b32 v227, v115 offset:512
	ds_read_b32 v228, v115 offset:1024
	ds_read_b32 v229, v115 offset:1536
	ds_read_b32 v230, v115 offset:2048
	ds_read_b32 v231, v115 offset:2560
	ds_read_b32 v232, v115 offset:3072
	ds_read_b32 v233, v115 offset:3584
	s_waitcnt lgkmcnt(0)
	v_bfe_u32 v120, v226, 16, 1
	v_bfe_u32 v121, v227, 16, 1
	v_bfe_u32 v122, v228, 16, 1
	v_bfe_u32 v123, v229, 16, 1
	v_bfe_u32 v124, v230, 16, 1
	v_bfe_u32 v125, v231, 16, 1
	v_bfe_u32 v126, v232, 16, 1
	v_bfe_u32 v127, v233, 16, 1
	v_add3_u32 v226, v226, v120, s63
	v_add3_u32 v227, v227, v121, s63
	v_add3_u32 v228, v228, v122, s63
	v_add3_u32 v229, v229, v123, s63
	v_add3_u32 v230, v230, v124, s63
	v_add3_u32 v231, v231, v125, s63
	v_add3_u32 v232, v232, v126, s63
	v_add3_u32 v233, v233, v127, s63
	v_perm_b32 v242, v227, v226, s64
	v_perm_b32 v243, v229, v228, s64
	v_perm_b32 v244, v231, v230, s64
	v_perm_b32 v245, v233, v232, s64
	s_nop 0
	global_store_dwordx4 v92, v[242:245], s[6:7]
	ds_read_b32 v226, v117
	ds_read_b32 v227, v117 offset:512
	ds_read_b32 v228, v117 offset:1024
	ds_read_b32 v229, v117 offset:1536
	ds_read_b32 v230, v117 offset:2048
	ds_read_b32 v231, v117 offset:2560
	ds_read_b32 v232, v117 offset:3072
	ds_read_b32 v233, v117 offset:3584
	s_waitcnt lgkmcnt(0)
	v_bfe_u32 v120, v226, 16, 1
	v_bfe_u32 v121, v227, 16, 1
	v_bfe_u32 v122, v228, 16, 1
	v_bfe_u32 v123, v229, 16, 1
	v_bfe_u32 v124, v230, 16, 1
	v_bfe_u32 v125, v231, 16, 1
	v_bfe_u32 v126, v232, 16, 1
	v_bfe_u32 v127, v233, 16, 1
	v_add3_u32 v226, v226, v120, s63
	v_add3_u32 v227, v227, v121, s63
	v_add3_u32 v228, v228, v122, s63
	v_add3_u32 v229, v229, v123, s63
	v_add3_u32 v230, v230, v124, s63
	v_add3_u32 v231, v231, v125, s63
	v_add3_u32 v232, v232, v126, s63
	v_add3_u32 v233, v233, v127, s63
	v_perm_b32 v242, v227, v226, s64
	v_perm_b32 v243, v229, v228, s64
	v_perm_b32 v244, v231, v230, s64
	v_perm_b32 v245, v233, v232, s64
	s_nop 0
	global_store_dwordx4 v93, v[242:245], s[6:7]
	ds_read_b32 v226, v119
	ds_read_b32 v227, v119 offset:512
	ds_read_b32 v228, v119 offset:1024
	ds_read_b32 v229, v119 offset:1536
	ds_read_b32 v230, v119 offset:2048
	ds_read_b32 v231, v119 offset:2560
	ds_read_b32 v232, v119 offset:3072
	ds_read_b32 v233, v119 offset:3584
	s_waitcnt lgkmcnt(0)
	v_bfe_u32 v120, v226, 16, 1
	v_bfe_u32 v121, v227, 16, 1
	v_bfe_u32 v122, v228, 16, 1
	v_bfe_u32 v123, v229, 16, 1
	v_bfe_u32 v124, v230, 16, 1
	v_bfe_u32 v125, v231, 16, 1
	v_bfe_u32 v126, v232, 16, 1
	v_bfe_u32 v127, v233, 16, 1
	v_add3_u32 v226, v226, v120, s63
	v_add3_u32 v227, v227, v121, s63
	v_add3_u32 v228, v228, v122, s63
	v_add3_u32 v229, v229, v123, s63
	v_add3_u32 v230, v230, v124, s63
	v_add3_u32 v231, v231, v125, s63
	v_add3_u32 v232, v232, v126, s63
	v_add3_u32 v233, v233, v127, s63
	v_perm_b32 v242, v227, v226, s64
	v_perm_b32 v243, v229, v228, s64
	v_perm_b32 v244, v231, v230, s64
	v_perm_b32 v245, v233, v232, s64
	s_nop 0
	global_store_dwordx4 v94, v[242:245], s[6:7]
	s_waitcnt vmcnt(16)
	v_mul_f32_e32 v144, v42, v144
	v_mul_f32_e32 v145, v42, v145
	v_mul_f32_e32 v146, v42, v146
	v_mul_f32_e32 v147, v42, v147
	ds_write_b128 v209, v[144:147]
	v_mul_f32_e32 v148, v43, v148
	v_mul_f32_e32 v149, v43, v149
	v_mul_f32_e32 v150, v43, v150
	v_mul_f32_e32 v151, v43, v151
	ds_write_b128 v209, v[148:151] offset:1024
	v_mul_f32_e32 v152, v44, v152
	v_mul_f32_e32 v153, v44, v153
	v_mul_f32_e32 v154, v44, v154
	v_mul_f32_e32 v155, v44, v155
	ds_write_b128 v209, v[152:155] offset:2048
	v_mul_f32_e32 v156, v45, v156
	v_mul_f32_e32 v157, v45, v157
	v_mul_f32_e32 v158, v45, v158
	v_mul_f32_e32 v159, v45, v159
	ds_write_b128 v209, v[156:159] offset:3072
	v_mul_f32_e32 v160, v46, v160
	v_mul_f32_e32 v161, v46, v161
	v_mul_f32_e32 v162, v46, v162
	v_mul_f32_e32 v163, v46, v163
	ds_write_b128 v209, v[160:163] offset:4096
	v_mul_f32_e32 v164, v47, v164
	v_mul_f32_e32 v165, v47, v165
	v_mul_f32_e32 v166, v47, v166
	v_mul_f32_e32 v167, v47, v167
	ds_write_b128 v209, v[164:167] offset:5120
	v_mul_f32_e32 v168, v48, v168
	v_mul_f32_e32 v169, v48, v169
	v_mul_f32_e32 v170, v48, v170
	v_mul_f32_e32 v171, v48, v171
	ds_write_b128 v209, v[168:171] offset:6144
	v_mul_f32_e32 v172, v49, v172
	v_mul_f32_e32 v173, v49, v173
	v_mul_f32_e32 v174, v49, v174
	v_mul_f32_e32 v175, v49, v175
	ds_write_b128 v209, v[172:175] offset:7168
	s_waitcnt lgkmcnt(0)
	s_barrier
; #define GAS __attribute__((address_space(1)))
; #define LAS __attribute__((address_space(3)))
; #define LDS_WAIT() asm volatile("s_waitcnt lgkmcnt(0)" ::: "memory")
; __device__ __forceinline__ unsigned pk2(float lo, float hi) { return f2bf(lo) | (f2bf(hi) << 16); }
; __device__ __forceinline__ int nat_dim(int p) { return (p >> 1) + 64 * (p & 1); }
; __device__ __forceinline__ int src_col_in(int c) {
;     if (c < 5120) { const int blk = c >> 7, p = c & 127; const bool rope = blk < 16 || ((((blk - 16) >> 2) & 1) == 0); const int d = rope ? (p >> 1) + 64 * (p & 1) : p; return blk * 128 + d; }
;     if (c < OFF_Z) return c + 2096;
;     if (c < OFF_G) return c - 4048;
;     if (c < OFF_DT) return 5120 + (c - OFF_G);
;     if (c < NSRC) return c;
;     return -1;
; template <int MAP, bool KS, bool KPERM = false>
; __device__ __forceinline__ void p0_transpose_item(const float* W, int K, int Nsrc, int nblk, bf16* WT, const float* ksA, const float* ksB, int ksplit, LAS float* scr, int item, int lane) {
;     const int kb = item / nblk, nb = item % nblk, k0 = 64 * kb, n0 = 32 * nb;
;     const int nr = n0 + (lane & 31); const int sc = MAP == 1 ? src_col_in(nr) : (MAP == 2 ? nat_dim(nr) : nr);
;     float v[32];
; #pragma unroll
;     for (int i = 0; i < 32; ++i) { const int k = k0 + 2 * i + (lane >> 5); const int ksrc = KPERM ? ((k & ~127) + nat_dim(k & 127)) : k;
;         v[i] = sc >= 0 ? W[(size_t)ksrc * Nsrc + sc] : 0.f; }
; #pragma unroll
;     for (int i = 0; i < 32; ++i) { const int kk = 2 * i + (lane >> 5); const int k = k0 + kk;
;         if (KS) v[i] *= (k < ksplit ? ksA[k] : ksB[k - ksplit]);
;         scr[kk * 33 + (lane & 31)] = v[i]; }
;     LDS_WAIT(); asm volatile("" ::: "memory");
;     const int c = lane & 7;
; #pragma unroll
;     for (int j = 0; j < 4; ++j) { const int n = (lane >> 3) + 8 * j; const LAS float* s = scr + (8 * c) * 33 + n;
;         v4u o; o.x = pk2(s[0 * 33], s[1 * 33]); o.y = pk2(s[2 * 33], s[3 * 33]); o.z = pk2(s[4 * 33], s[5 * 33]); o.w = pk2(s[6 * 33], s[7 * 33]);
;         *(GAS v4u*)(WT + (size_t)(n0 + n) * K + k0 + 8 * c) = o; }
;     LDS_WAIT(); asm volatile("" ::: "memory");
	s_add_i32 s24, s23, 8
	s_lshl_b32 s20, s24, 7
	s_cmp_lt_u32 s24, 40
	s_cselect_b32 s21, 0, 0x830
	s_cmp_lt_u32 s24, 72
	s_cselect_b32 s21, s21, 0xfffff030
	s_add_i32 s20, s20, s21
	s_lshl_b32 s20, s20, 2
	s_add_u32 s8, s50, s20
	s_addc_u32 s9, s51, 0
	global_load_dwordx4 v[144:147], v76, s[8:9]
	s_add_u32 s8, s8, 0x16280
	s_addc_u32 s9, s9, 0
	global_load_dwordx4 v[148:151], v76, s[8:9]
	s_add_u32 s8, s8, 0x16280
	s_addc_u32 s9, s9, 0
	global_load_dwordx4 v[152:155], v76, s[8:9]
	s_add_u32 s8, s8, 0x16280
	s_addc_u32 s9, s9, 0
	global_load_dwordx4 v[156:159], v76, s[8:9]
	s_add_u32 s8, s8, 0x16280
	s_addc_u32 s9, s9, 0
	global_load_dwordx4 v[160:163], v76, s[8:9]
	s_add_u32 s8, s8, 0x16280
	s_addc_u32 s9, s9, 0
	global_load_dwordx4 v[164:167], v76, s[8:9]
	s_add_u32 s8, s8, 0x16280
	s_addc_u32 s9, s9, 0
	global_load_dwordx4 v[168:171], v76, s[8:9]
	s_add_u32 s8, s8, 0x16280
	s_addc_u32 s9, s9, 0
	global_load_dwordx4 v[172:175], v76, s[8:9]
	s_add_i32 s24, s23, 80
	s_mul_i32 s20, s24, 0x100000
	s_add_u32 s6, s48, s20
	s_addc_u32 s7, s49, 0
	s_cmp_lt_u32 s24, 16
	s_cselect_b32 s20, 1, 0
	s_sub_i32 s21, s24, 16
	s_bitcmp0_b32 s21, 2
	s_cselect_b32 s21, 1, 0
	s_cmp_lt_u32 s24, 40
	s_cselect_b32 s21, s21, 0
	s_or_b32 s20, s20, s21
	s_cmp_lg_u32 s20, 0
	s_cselect_b64 s[20:21], -1, 0
	v_cndmask_b32_e64 v91, v83, v87, s[20:21]
	v_cndmask_b32_e64 v92, v84, v88, s[20:21]
	v_cndmask_b32_e64 v93, v85, v89, s[20:21]
	v_cndmask_b32_e64 v94, v86, v90, s[20:21]
	ds_read_b32 v226, v112
	ds_read_b32 v227, v112 offset:512
	ds_read_b32 v228, v112 offset:1024
	ds_read_b32 v229, v112 offset:1536
	ds_read_b32 v230, v112 offset:2048
	ds_read_b32 v231, v112 offset:2560
	ds_read_b32 v232, v112 offset:3072
	ds_read_b32 v233, v112 offset:3584
	s_waitcnt lgkmcnt(0)
	v_bfe_u32 v120, v226, 16, 1
	v_bfe_u32 v121, v227, 16, 1
	v_bfe_u32 v122, v228, 16, 1
	v_bfe_u32 v123, v229, 16, 1
	v_bfe_u32 v124, v230, 16, 1
	v_bfe_u32 v125, v231, 16, 1
	v_bfe_u32 v126, v232, 16, 1
	v_bfe_u32 v127, v233, 16, 1
	v_add3_u32 v226, v226, v120, s63
	v_add3_u32 v227, v227, v121, s63
	v_add3_u32 v228, v228, v122, s63
	v_add3_u32 v229, v229, v123, s63
	v_add3_u32 v230, v230, v124, s63
	v_add3_u32 v231, v231, v125, s63
	v_add3_u32 v232, v232, v126, s63
	v_add3_u32 v233, v233, v127, s63
	v_perm_b32 v242, v227, v226, s64
	v_perm_b32 v243, v229, v228, s64
	v_perm_b32 v244, v231, v230, s64
	v_perm_b32 v245, v233, v232, s64
	s_nop 0
	global_store_dwordx4 v91, v[242:245], s[6:7]
	ds_read_b32 v226, v114
	ds_read_b32 v227, v114 offset:512
	ds_read_b32 v228, v114 offset:1024
	ds_read_b32 v229, v114 offset:1536
	ds_read_b32 v230, v114 offset:2048
	ds_read_b32 v231, v114 offset:2560
	ds_read_b32 v232, v114 offset:3072
	ds_read_b32 v233, v114 offset:3584
	s_waitcnt lgkmcnt(0)
	v_bfe_u32 v120, v226, 16, 1
	v_bfe_u32 v121, v227, 16, 1
	v_bfe_u32 v122, v228, 16, 1
	v_bfe_u32 v123, v229, 16, 1
	v_bfe_u32 v124, v230, 16, 1
	v_bfe_u32 v125, v231, 16, 1
	v_bfe_u32 v126, v232, 16, 1
	v_bfe_u32 v127, v233, 16, 1
	v_add3_u32 v226, v226, v120, s63
	v_add3_u32 v227, v227, v121, s63
	v_add3_u32 v228, v228, v122, s63
	v_add3_u32 v229, v229, v123, s63
	v_add3_u32 v230, v230, v124, s63
	v_add3_u32 v231, v231, v125, s63
	v_add3_u32 v232, v232, v126, s63
	v_add3_u32 v233, v233, v127, s63
	v_perm_b32 v242, v227, v226, s64
	v_perm_b32 v243, v229, v228, s64
	v_perm_b32 v244, v231, v230, s64
	v_perm_b32 v245, v233, v232, s64
	s_nop 0
	global_store_dwordx4 v92, v[242:245], s[6:7]
	ds_read_b32 v226, v116
	ds_read_b32 v227, v116 offset:512
	ds_read_b32 v228, v116 offset:1024
	ds_read_b32 v229, v116 offset:1536
	ds_read_b32 v230, v116 offset:2048
	ds_read_b32 v231, v116 offset:2560
	ds_read_b32 v232, v116 offset:3072
	ds_read_b32 v233, v116 offset:3584
	s_waitcnt lgkmcnt(0)
	v_bfe_u32 v120, v226, 16, 1
	v_bfe_u32 v121, v227, 16, 1
	v_bfe_u32 v122, v228, 16, 1
	v_bfe_u32 v123, v229, 16, 1
	v_bfe_u32 v124, v230, 16, 1
	v_bfe_u32 v125, v231, 16, 1
	v_bfe_u32 v126, v232, 16, 1
	v_bfe_u32 v127, v233, 16, 1
	v_add3_u32 v226, v226, v120, s63
	v_add3_u32 v227, v227, v121, s63
	v_add3_u32 v228, v228, v122, s63
	v_add3_u32 v229, v229, v123, s63
	v_add3_u32 v230, v230, v124, s63
	v_add3_u32 v231, v231, v125, s63
	v_add3_u32 v232, v232, v126, s63
	v_add3_u32 v233, v233, v127, s63
	v_perm_b32 v242, v227, v226, s64
	v_perm_b32 v243, v229, v228, s64
	v_perm_b32 v244, v231, v230, s64
	v_perm_b32 v245, v233, v232, s64
	s_nop 0
	global_store_dwordx4 v93, v[242:245], s[6:7]
	ds_read_b32 v226, v118
	ds_read_b32 v227, v118 offset:512
	ds_read_b32 v228, v118 offset:1024
	ds_read_b32 v229, v118 offset:1536
	ds_read_b32 v230, v118 offset:2048
	ds_read_b32 v231, v118 offset:2560
	ds_read_b32 v232, v118 offset:3072
	ds_read_b32 v233, v118 offset:3584
	s_waitcnt lgkmcnt(0)
	v_bfe_u32 v120, v226, 16, 1
	v_bfe_u32 v121, v227, 16, 1
	v_bfe_u32 v122, v228, 16, 1
	v_bfe_u32 v123, v229, 16, 1
	v_bfe_u32 v124, v230, 16, 1
	v_bfe_u32 v125, v231, 16, 1
	v_bfe_u32 v126, v232, 16, 1
	v_bfe_u32 v127, v233, 16, 1
	v_add3_u32 v226, v226, v120, s63
	v_add3_u32 v227, v227, v121, s63
	v_add3_u32 v228, v228, v122, s63
	v_add3_u32 v229, v229, v123, s63
	v_add3_u32 v230, v230, v124, s63
	v_add3_u32 v231, v231, v125, s63
	v_add3_u32 v232, v232, v126, s63
	v_add3_u32 v233, v233, v127, s63
	v_perm_b32 v242, v227, v226, s64
	v_perm_b32 v243, v229, v228, s64
	v_perm_b32 v244, v231, v230, s64
	v_perm_b32 v245, v233, v232, s64
	s_nop 0
	global_store_dwordx4 v94, v[242:245], s[6:7]
	s_waitcnt vmcnt(16)
	v_mul_f32_e32 v176, v50, v176
	v_mul_f32_e32 v177, v50, v177
	v_mul_f32_e32 v178, v50, v178
	v_mul_f32_e32 v179, v50, v179
	ds_write_b128 v210, v[176:179]
	v_mul_f32_e32 v180, v51, v180
	v_mul_f32_e32 v181, v51, v181
	v_mul_f32_e32 v182, v51, v182
	v_mul_f32_e32 v183, v51, v183
	ds_write_b128 v210, v[180:183] offset:1024
	v_mul_f32_e32 v184, v52, v184
	v_mul_f32_e32 v185, v52, v185
	v_mul_f32_e32 v186, v52, v186
	v_mul_f32_e32 v187, v52, v187
	ds_write_b128 v210, v[184:187] offset:2048
	v_mul_f32_e32 v188, v53, v188
	v_mul_f32_e32 v189, v53, v189
	v_mul_f32_e32 v190, v53, v190
	v_mul_f32_e32 v191, v53, v191
	ds_write_b128 v210, v[188:191] offset:3072
	v_mul_f32_e32 v192, v54, v192
	v_mul_f32_e32 v193, v54, v193
	v_mul_f32_e32 v194, v54, v194
	v_mul_f32_e32 v195, v54, v195
	ds_write_b128 v210, v[192:195] offset:4096
	v_mul_f32_e32 v196, v55, v196
	v_mul_f32_e32 v197, v55, v197
	v_mul_f32_e32 v198, v55, v198
	v_mul_f32_e32 v199, v55, v199
	ds_write_b128 v210, v[196:199] offset:5120
	v_mul_f32_e32 v200, v56, v200
	v_mul_f32_e32 v201, v56, v201
	v_mul_f32_e32 v202, v56, v202
	v_mul_f32_e32 v203, v56, v203
	ds_write_b128 v210, v[200:203] offset:6144
	v_mul_f32_e32 v204, v57, v204
	v_mul_f32_e32 v205, v57, v205
	v_mul_f32_e32 v206, v57, v206
	v_mul_f32_e32 v207, v57, v207
	ds_write_b128 v210, v[204:207] offset:7168
	s_waitcnt lgkmcnt(0)
	s_barrier
; #define GAS __attribute__((address_space(1)))
; #define LAS __attribute__((address_space(3)))
; #define LDS_WAIT() asm volatile("s_waitcnt lgkmcnt(0)" ::: "memory")
; __device__ __forceinline__ int src_col_in(int c) {
;     if (c < 5120) { const int blk = c >> 7, p = c & 127; const bool rope = blk < 16 || ((((blk - 16) >> 2) & 1) == 0); const int d = rope ? (p >> 1) + 64 * (p & 1) : p; return blk * 128 + d; }
;     if (c < OFF_Z) return c + 2096;
;     if (c < OFF_G) return c - 4048;
;     if (c < OFF_DT) return 5120 + (c - OFF_G);
;     if (c < NSRC) return c;
;     return -1;
;     const int pr = item >> 1, kb = 2 * (pr / nblk) + (item & 1), nb = pr % nblk, k0 = 64 * kb, n0 = 32 * nb;
;     const int nr = n0 + (lane & 31); const int sc = MAP == 1 ? src_col_in(nr) : nr;
;     float v[32];
; #pragma unroll
;     for (int i = 0; i < 32; ++i) v[i] = sc >= 0 ? W[(size_t)(k0 + 2 * i + (lane >> 5)) * Nsrc + sc] : 0.f;
; #pragma unroll
;     for (int i = 0; i < 32; ++i) { const int k = k0 + 2 * i + (lane >> 5); float x = v[i] * wscale; if (KS) x *= (k < ksplit ? ksA[k] : ksB[k - ksplit]); scr[(2 * i + (lane >> 5)) * 33 + (lane & 31)] = x; }
;     LDS_WAIT(); asm volatile("" ::: "memory");
;     const int c = lane & 7;
; #pragma unroll
;     for (int j = 0; j < 4; ++j) { const int n = (lane >> 3) + 8 * j; const LAS float* s = scr + (8 * c) * 33 + n;
;         const unsigned long long o = (unsigned long long)pg8::pk4_fp8(s[0 * 33], s[1 * 33], s[2 * 33], s[3 * 33]) | ((unsigned long long)pg8::pk4_fp8(s[4 * 33], s[5 * 33], s[6 * 33], s[7 * 33]) << 32);
;         *(GAS unsigned long long*)(WT + (size_t)(n0 + n) * K + k0 + 8 * c) = o; }
;     LDS_WAIT(); asm volatile("" ::: "memory");
	s_add_i32 s24, s23, 16
	s_lshl_b32 s20, s24, 7
	s_cmp_lt_u32 s24, 40
	s_cselect_b32 s21, 0, 0x830
	s_cmp_lt_u32 s24, 72
	s_cselect_b32 s21, s21, 0xfffff030
	s_add_i32 s20, s20, s21
	s_lshl_b32 s20, s20, 2
	s_add_u32 s8, s50, s20
	s_addc_u32 s9, s51, 0
	global_load_dwordx4 v[176:179], v76, s[8:9]
	s_add_u32 s8, s8, 0x16280
	s_addc_u32 s9, s9, 0
	global_load_dwordx4 v[180:183], v76, s[8:9]
	s_add_u32 s8, s8, 0x16280
	s_addc_u32 s9, s9, 0
	global_load_dwordx4 v[184:187], v76, s[8:9]
	s_add_u32 s8, s8, 0x16280
	s_addc_u32 s9, s9, 0
	global_load_dwordx4 v[188:191], v76, s[8:9]
	s_add_u32 s8, s8, 0x16280
	s_addc_u32 s9, s9, 0
	global_load_dwordx4 v[192:195], v76, s[8:9]
	s_add_u32 s8, s8, 0x16280
	s_addc_u32 s9, s9, 0
	global_load_dwordx4 v[196:199], v76, s[8:9]
	s_add_u32 s8, s8, 0x16280
	s_addc_u32 s9, s9, 0
	global_load_dwordx4 v[200:203], v76, s[8:9]
	s_add_u32 s8, s8, 0x16280
	s_addc_u32 s9, s9, 0
	global_load_dwordx4 v[204:207], v76, s[8:9]
	s_add_i32 s24, s23, 0
	s_mul_i32 s20, s24, 0x80000
	s_add_u32 s6, s52, s20
	s_addc_u32 s7, s53, 0
	s_cmp_lt_u32 s24, 16
	s_cselect_b32 s20, 1, 0
	s_sub_i32 s21, s24, 16
	s_bitcmp0_b32 s21, 2
	s_cselect_b32 s21, 1, 0
	s_cmp_lt_u32 s24, 40
	s_cselect_b32 s21, s21, 0
	s_or_b32 s20, s20, s21
	s_cmp_lg_u32 s20, 0
	s_cselect_b64 s[20:21], -1, 0
	v_cndmask_b32_e64 v91, v77, v81, s[20:21]
	v_cndmask_b32_e64 v92, v78, v82, s[20:21]
	ds_read_b32 v226, v212
	ds_read_b32 v227, v212 offset:512
	ds_read_b32 v228, v212 offset:1024
	ds_read_b32 v229, v212 offset:1536
	ds_read_b32 v230, v212 offset:2048
	ds_read_b32 v231, v212 offset:2560
	ds_read_b32 v232, v212 offset:3072
	ds_read_b32 v233, v212 offset:3584
	ds_read_b32 v234, v212 offset:4096
	ds_read_b32 v235, v212 offset:4608
	ds_read_b32 v236, v212 offset:5120
	ds_read_b32 v237, v212 offset:5632
	ds_read_b32 v238, v212 offset:6144
	ds_read_b32 v239, v212 offset:6656
	ds_read_b32 v240, v212 offset:7168
	ds_read_b32 v241, v212 offset:7680
	s_waitcnt lgkmcnt(0)
	v_max_f32_e32 v226, v226, v226
	v_max_f32_e32 v227, v227, v227
	v_max_f32_e32 v228, v228, v228
	v_max_f32_e32 v229, v229, v229
	v_max_f32_e32 v230, v230, v230
	v_max_f32_e32 v231, v231, v231
	v_max_f32_e32 v232, v232, v232
	v_max_f32_e32 v233, v233, v233
	v_max_f32_e32 v234, v234, v234
	v_max_f32_e32 v235, v235, v235
	v_max_f32_e32 v236, v236, v236
	v_max_f32_e32 v237, v237, v237
	v_max_f32_e32 v238, v238, v238
	v_max_f32_e32 v239, v239, v239
	v_max_f32_e32 v240, v240, v240
	v_max_f32_e32 v241, v241, v241
	v_med3_f32 v226, v226, s62, v95
	v_med3_f32 v227, v227, s62, v95
	v_med3_f32 v228, v228, s62, v95
	v_med3_f32 v229, v229, s62, v95
	v_med3_f32 v230, v230, s62, v95
	v_med3_f32 v231, v231, s62, v95
	v_med3_f32 v232, v232, s62, v95
	v_med3_f32 v233, v233, s62, v95
	v_med3_f32 v234, v234, s62, v95
	v_med3_f32 v235, v235, s62, v95
	v_med3_f32 v236, v236, s62, v95
	v_med3_f32 v237, v237, s62, v95
	v_med3_f32 v238, v238, s62, v95
	v_med3_f32 v239, v239, s62, v95
	v_med3_f32 v240, v240, s62, v95
	v_med3_f32 v241, v241, s62, v95
	v_mov_b32_e32 v242, 0
	v_mov_b32_e32 v243, 0
	v_mov_b32_e32 v244, 0
	v_mov_b32_e32 v245, 0
	v_cvt_pk_fp8_f32 v242, v226, v227
	v_cvt_pk_fp8_f32 v243, v230, v231
	v_cvt_pk_fp8_f32 v244, v234, v235
	v_cvt_pk_fp8_f32 v245, v238, v239
	v_cvt_pk_fp8_f32 v242, v228, v229 op_sel:[0,0,1]
	v_cvt_pk_fp8_f32 v243, v232, v233 op_sel:[0,0,1]
	v_cvt_pk_fp8_f32 v244, v236, v237 op_sel:[0,0,1]
	v_cvt_pk_fp8_f32 v245, v240, v241 op_sel:[0,0,1]
	s_nop 0
	global_store_dwordx4 v91, v[242:245], s[6:7]
	ds_read_b32 v226, v214
	ds_read_b32 v227, v214 offset:512
	ds_read_b32 v228, v214 offset:1024
	ds_read_b32 v229, v214 offset:1536
	ds_read_b32 v230, v214 offset:2048
	ds_read_b32 v231, v214 offset:2560
	ds_read_b32 v232, v214 offset:3072
	ds_read_b32 v233, v214 offset:3584
	ds_read_b32 v234, v214 offset:4096
	ds_read_b32 v235, v214 offset:4608
	ds_read_b32 v236, v214 offset:5120
	ds_read_b32 v237, v214 offset:5632
	ds_read_b32 v238, v214 offset:6144
	ds_read_b32 v239, v214 offset:6656
	ds_read_b32 v240, v214 offset:7168
	ds_read_b32 v241, v214 offset:7680
	s_waitcnt lgkmcnt(0)
	v_max_f32_e32 v226, v226, v226
	v_max_f32_e32 v227, v227, v227
	v_max_f32_e32 v228, v228, v228
	v_max_f32_e32 v229, v229, v229
	v_max_f32_e32 v230, v230, v230
	v_max_f32_e32 v231, v231, v231
	v_max_f32_e32 v232, v232, v232
	v_max_f32_e32 v233, v233, v233
	v_max_f32_e32 v234, v234, v234
	v_max_f32_e32 v235, v235, v235
	v_max_f32_e32 v236, v236, v236
	v_max_f32_e32 v237, v237, v237
	v_max_f32_e32 v238, v238, v238
	v_max_f32_e32 v239, v239, v239
	v_max_f32_e32 v240, v240, v240
	v_max_f32_e32 v241, v241, v241
	v_med3_f32 v226, v226, s62, v95
	v_med3_f32 v227, v227, s62, v95
	v_med3_f32 v228, v228, s62, v95
	v_med3_f32 v229, v229, s62, v95
	v_med3_f32 v230, v230, s62, v95
	v_med3_f32 v231, v231, s62, v95
	v_med3_f32 v232, v232, s62, v95
	v_med3_f32 v233, v233, s62, v95
	v_med3_f32 v234, v234, s62, v95
	v_med3_f32 v235, v235, s62, v95
	v_med3_f32 v236, v236, s62, v95
	v_med3_f32 v237, v237, s62, v95
	v_med3_f32 v238, v238, s62, v95
	v_med3_f32 v239, v239, s62, v95
	v_med3_f32 v240, v240, s62, v95
	v_med3_f32 v241, v241, s62, v95
	v_mov_b32_e32 v242, 0
	v_mov_b32_e32 v243, 0
	v_mov_b32_e32 v244, 0
	v_mov_b32_e32 v245, 0
	v_cvt_pk_fp8_f32 v242, v226, v227
	v_cvt_pk_fp8_f32 v243, v230, v231
	v_cvt_pk_fp8_f32 v244, v234, v235
	v_cvt_pk_fp8_f32 v245, v238, v239
	v_cvt_pk_fp8_f32 v242, v228, v229 op_sel:[0,0,1]
	v_cvt_pk_fp8_f32 v243, v232, v233 op_sel:[0,0,1]
	v_cvt_pk_fp8_f32 v244, v236, v237 op_sel:[0,0,1]
	v_cvt_pk_fp8_f32 v245, v240, v241 op_sel:[0,0,1]
	s_nop 0
	global_store_dwordx4 v92, v[242:245], s[6:7]
	s_waitcnt vmcnt(14)
	v_mul_f32_e32 v144, v50, v144
	v_mul_f32_e32 v145, v50, v145
	v_mul_f32_e32 v146, v50, v146
	v_mul_f32_e32 v147, v50, v147
	ds_write_b128 v209, v[144:147]
	v_mul_f32_e32 v148, v51, v148
	v_mul_f32_e32 v149, v51, v149
	v_mul_f32_e32 v150, v51, v150
	v_mul_f32_e32 v151, v51, v151
	ds_write_b128 v209, v[148:151] offset:1024
	v_mul_f32_e32 v152, v52, v152
	v_mul_f32_e32 v153, v52, v153
	v_mul_f32_e32 v154, v52, v154
	v_mul_f32_e32 v155, v52, v155
	ds_write_b128 v209, v[152:155] offset:2048
	v_mul_f32_e32 v156, v53, v156
	v_mul_f32_e32 v157, v53, v157
	v_mul_f32_e32 v158, v53, v158
	v_mul_f32_e32 v159, v53, v159
	ds_write_b128 v209, v[156:159] offset:3072
	v_mul_f32_e32 v160, v54, v160
	v_mul_f32_e32 v161, v54, v161
	v_mul_f32_e32 v162, v54, v162
	v_mul_f32_e32 v163, v54, v163
	ds_write_b128 v209, v[160:163] offset:4096
	v_mul_f32_e32 v164, v55, v164
	v_mul_f32_e32 v165, v55, v165
	v_mul_f32_e32 v166, v55, v166
	v_mul_f32_e32 v167, v55, v167
	ds_write_b128 v209, v[164:167] offset:5120
	v_mul_f32_e32 v168, v56, v168
	v_mul_f32_e32 v169, v56, v169
	v_mul_f32_e32 v170, v56, v170
	v_mul_f32_e32 v171, v56, v171
	ds_write_b128 v209, v[168:171] offset:6144
	v_mul_f32_e32 v172, v57, v172
	v_mul_f32_e32 v173, v57, v173
	v_mul_f32_e32 v174, v57, v174
	v_mul_f32_e32 v175, v57, v175
	ds_write_b128 v209, v[172:175] offset:7168
	s_waitcnt lgkmcnt(0)
	s_barrier
; #define GAS __attribute__((address_space(1)))
; #define LAS __attribute__((address_space(3)))
; #define LDS_WAIT() asm volatile("s_waitcnt lgkmcnt(0)" ::: "memory")
; __device__ __forceinline__ int src_col_in(int c) {
;     if (c < 5120) { const int blk = c >> 7, p = c & 127; const bool rope = blk < 16 || ((((blk - 16) >> 2) & 1) == 0); const int d = rope ? (p >> 1) + 64 * (p & 1) : p; return blk * 128 + d; }
;     if (c < OFF_Z) return c + 2096;
;     if (c < OFF_G) return c - 4048;
;     if (c < OFF_DT) return 5120 + (c - OFF_G);
;     if (c < NSRC) return c;
;     return -1;
;     const int pr = item >> 1, kb = 2 * (pr / nblk) + (item & 1), nb = pr % nblk, k0 = 64 * kb, n0 = 32 * nb;
;     const int nr = n0 + (lane & 31); const int sc = MAP == 1 ? src_col_in(nr) : nr;
;     float v[32];
; #pragma unroll
;     for (int i = 0; i < 32; ++i) v[i] = sc >= 0 ? W[(size_t)(k0 + 2 * i + (lane >> 5)) * Nsrc + sc] : 0.f;
; #pragma unroll
;     for (int i = 0; i < 32; ++i) { const int k = k0 + 2 * i + (lane >> 5); float x = v[i] * wscale; if (KS) x *= (k < ksplit ? ksA[k] : ksB[k - ksplit]); scr[(2 * i + (lane >> 5)) * 33 + (lane & 31)] = x; }
;     LDS_WAIT(); asm volatile("" ::: "memory");
;     const int c = lane & 7;
; #pragma unroll
;     for (int j = 0; j < 4; ++j) { const int n = (lane >> 3) + 8 * j; const LAS float* s = scr + (8 * c) * 33 + n;
;         const unsigned long long o = (unsigned long long)pg8::pk4_fp8(s[0 * 33], s[1 * 33], s[2 * 33], s[3 * 33]) | ((unsigned long long)pg8::pk4_fp8(s[4 * 33], s[5 * 33], s[6 * 33], s[7 * 33]) << 32);
;         *(GAS unsigned long long*)(WT + (size_t)(n0 + n) * K + k0 + 8 * c) = o; }
;     LDS_WAIT(); asm volatile("" ::: "memory");
	s_add_i32 s24, s23, 24
	s_lshl_b32 s20, s24, 7
	s_cmp_lt_u32 s24, 40
	s_cselect_b32 s21, 0, 0x830
	s_cmp_lt_u32 s24, 72
	s_cselect_b32 s21, s21, 0xfffff030
	s_add_i32 s20, s20, s21
	s_lshl_b32 s20, s20, 2
	s_add_u32 s8, s50, s20
	s_addc_u32 s9, s51, 0
	global_load_dwordx4 v[144:147], v76, s[8:9]
	s_add_u32 s8, s8, 0x16280
	s_addc_u32 s9, s9, 0
	global_load_dwordx4 v[148:151], v76, s[8:9]
	s_add_u32 s8, s8, 0x16280
	s_addc_u32 s9, s9, 0
	global_load_dwordx4 v[152:155], v76, s[8:9]
	s_add_u32 s8, s8, 0x16280
	s_addc_u32 s9, s9, 0
	global_load_dwordx4 v[156:159], v76, s[8:9]
	s_add_u32 s8, s8, 0x16280
	s_addc_u32 s9, s9, 0
	global_load_dwordx4 v[160:163], v76, s[8:9]
	s_add_u32 s8, s8, 0x16280
	s_addc_u32 s9, s9, 0
	global_load_dwordx4 v[164:167], v76, s[8:9]
	s_add_u32 s8, s8, 0x16280
	s_addc_u32 s9, s9, 0
	global_load_dwordx4 v[168:171], v76, s[8:9]
	s_add_u32 s8, s8, 0x16280
	s_addc_u32 s9, s9, 0
	global_load_dwordx4 v[172:175], v76, s[8:9]
	s_add_i32 s24, s23, 8
	s_mul_i32 s20, s24, 0x80000
	s_add_u32 s6, s52, s20
	s_addc_u32 s7, s53, 0
	s_cmp_lt_u32 s24, 16
	s_cselect_b32 s20, 1, 0
	s_sub_i32 s21, s24, 16
	s_bitcmp0_b32 s21, 2
	s_cselect_b32 s21, 1, 0
	s_cmp_lt_u32 s24, 40
	s_cselect_b32 s21, s21, 0
	s_or_b32 s20, s20, s21
	s_cmp_lg_u32 s20, 0
	s_cselect_b64 s[20:21], -1, 0
	v_cndmask_b32_e64 v91, v77, v81, s[20:21]
	v_cndmask_b32_e64 v92, v78, v82, s[20:21]
	ds_read_b32 v226, v211
	ds_read_b32 v227, v211 offset:512
	ds_read_b32 v228, v211 offset:1024
	ds_read_b32 v229, v211 offset:1536
	ds_read_b32 v230, v211 offset:2048
	ds_read_b32 v231, v211 offset:2560
	ds_read_b32 v232, v211 offset:3072
	ds_read_b32 v233, v211 offset:3584
	ds_read_b32 v234, v211 offset:4096
	ds_read_b32 v235, v211 offset:4608
	ds_read_b32 v236, v211 offset:5120
	ds_read_b32 v237, v211 offset:5632
	ds_read_b32 v238, v211 offset:6144
	ds_read_b32 v239, v211 offset:6656
	ds_read_b32 v240, v211 offset:7168
	ds_read_b32 v241, v211 offset:7680
	s_waitcnt lgkmcnt(0)
	v_max_f32_e32 v226, v226, v226
	v_max_f32_e32 v227, v227, v227
	v_max_f32_e32 v228, v228, v228
	v_max_f32_e32 v229, v229, v229
	v_max_f32_e32 v230, v230, v230
	v_max_f32_e32 v231, v231, v231
	v_max_f32_e32 v232, v232, v232
	v_max_f32_e32 v233, v233, v233
	v_max_f32_e32 v234, v234, v234
	v_max_f32_e32 v235, v235, v235
	v_max_f32_e32 v236, v236, v236
	v_max_f32_e32 v237, v237, v237
	v_max_f32_e32 v238, v238, v238
	v_max_f32_e32 v239, v239, v239
	v_max_f32_e32 v240, v240, v240
	v_max_f32_e32 v241, v241, v241
	v_med3_f32 v226, v226, s62, v95
	v_med3_f32 v227, v227, s62, v95
	v_med3_f32 v228, v228, s62, v95
	v_med3_f32 v229, v229, s62, v95
	v_med3_f32 v230, v230, s62, v95
	v_med3_f32 v231, v231, s62, v95
	v_med3_f32 v232, v232, s62, v95
	v_med3_f32 v233, v233, s62, v95
	v_med3_f32 v234, v234, s62, v95
	v_med3_f32 v235, v235, s62, v95
	v_med3_f32 v236, v236, s62, v95
	v_med3_f32 v237, v237, s62, v95
	v_med3_f32 v238, v238, s62, v95
	v_med3_f32 v239, v239, s62, v95
	v_med3_f32 v240, v240, s62, v95
	v_med3_f32 v241, v241, s62, v95
	v_mov_b32_e32 v242, 0
	v_mov_b32_e32 v243, 0
	v_mov_b32_e32 v244, 0
	v_mov_b32_e32 v245, 0
	v_cvt_pk_fp8_f32 v242, v226, v227
	v_cvt_pk_fp8_f32 v243, v230, v231
	v_cvt_pk_fp8_f32 v244, v234, v235
	v_cvt_pk_fp8_f32 v245, v238, v239
	v_cvt_pk_fp8_f32 v242, v228, v229 op_sel:[0,0,1]
	v_cvt_pk_fp8_f32 v243, v232, v233 op_sel:[0,0,1]
	v_cvt_pk_fp8_f32 v244, v236, v237 op_sel:[0,0,1]
	v_cvt_pk_fp8_f32 v245, v240, v241 op_sel:[0,0,1]
	s_nop 0
	global_store_dwordx4 v91, v[242:245], s[6:7]
	ds_read_b32 v226, v213
	ds_read_b32 v227, v213 offset:512
	ds_read_b32 v228, v213 offset:1024
	ds_read_b32 v229, v213 offset:1536
	ds_read_b32 v230, v213 offset:2048
	ds_read_b32 v231, v213 offset:2560
	ds_read_b32 v232, v213 offset:3072
	ds_read_b32 v233, v213 offset:3584
	ds_read_b32 v234, v213 offset:4096
	ds_read_b32 v235, v213 offset:4608
	ds_read_b32 v236, v213 offset:5120
	ds_read_b32 v237, v213 offset:5632
	ds_read_b32 v238, v213 offset:6144
	ds_read_b32 v239, v213 offset:6656
	ds_read_b32 v240, v213 offset:7168
	ds_read_b32 v241, v213 offset:7680
	s_waitcnt lgkmcnt(0)
	v_max_f32_e32 v226, v226, v226
	v_max_f32_e32 v227, v227, v227
	v_max_f32_e32 v228, v228, v228
	v_max_f32_e32 v229, v229, v229
	v_max_f32_e32 v230, v230, v230
	v_max_f32_e32 v231, v231, v231
	v_max_f32_e32 v232, v232, v232
	v_max_f32_e32 v233, v233, v233
	v_max_f32_e32 v234, v234, v234
	v_max_f32_e32 v235, v235, v235
	v_max_f32_e32 v236, v236, v236
	v_max_f32_e32 v237, v237, v237
	v_max_f32_e32 v238, v238, v238
	v_max_f32_e32 v239, v239, v239
	v_max_f32_e32 v240, v240, v240
	v_max_f32_e32 v241, v241, v241
	v_med3_f32 v226, v226, s62, v95
	v_med3_f32 v227, v227, s62, v95
	v_med3_f32 v228, v228, s62, v95
	v_med3_f32 v229, v229, s62, v95
	v_med3_f32 v230, v230, s62, v95
	v_med3_f32 v231, v231, s62, v95
	v_med3_f32 v232, v232, s62, v95
	v_med3_f32 v233, v233, s62, v95
	v_med3_f32 v234, v234, s62, v95
	v_med3_f32 v235, v235, s62, v95
	v_med3_f32 v236, v236, s62, v95
	v_med3_f32 v237, v237, s62, v95
	v_med3_f32 v238, v238, s62, v95
	v_med3_f32 v239, v239, s62, v95
	v_med3_f32 v240, v240, s62, v95
	v_med3_f32 v241, v241, s62, v95
	v_mov_b32_e32 v242, 0
	v_mov_b32_e32 v243, 0
	v_mov_b32_e32 v244, 0
	v_mov_b32_e32 v245, 0
	v_cvt_pk_fp8_f32 v242, v226, v227
	v_cvt_pk_fp8_f32 v243, v230, v231
	v_cvt_pk_fp8_f32 v244, v234, v235
	v_cvt_pk_fp8_f32 v245, v238, v239
	v_cvt_pk_fp8_f32 v242, v228, v229 op_sel:[0,0,1]
	v_cvt_pk_fp8_f32 v243, v232, v233 op_sel:[0,0,1]
	v_cvt_pk_fp8_f32 v244, v236, v237 op_sel:[0,0,1]
	v_cvt_pk_fp8_f32 v245, v240, v241 op_sel:[0,0,1]
	s_nop 0
	global_store_dwordx4 v92, v[242:245], s[6:7]
	s_waitcnt vmcnt(12)
	v_mul_f32_e32 v176, v50, v176
	v_mul_f32_e32 v177, v50, v177
	v_mul_f32_e32 v178, v50, v178
	v_mul_f32_e32 v179, v50, v179
	ds_write_b128 v210, v[176:179]
	v_mul_f32_e32 v180, v51, v180
	v_mul_f32_e32 v181, v51, v181
	v_mul_f32_e32 v182, v51, v182
	v_mul_f32_e32 v183, v51, v183
	ds_write_b128 v210, v[180:183] offset:1024
	v_mul_f32_e32 v184, v52, v184
	v_mul_f32_e32 v185, v52, v185
	v_mul_f32_e32 v186, v52, v186
	v_mul_f32_e32 v187, v52, v187
	ds_write_b128 v210, v[184:187] offset:2048
	v_mul_f32_e32 v188, v53, v188
	v_mul_f32_e32 v189, v53, v189
	v_mul_f32_e32 v190, v53, v190
	v_mul_f32_e32 v191, v53, v191
	ds_write_b128 v210, v[188:191] offset:3072
	v_mul_f32_e32 v192, v54, v192
	v_mul_f32_e32 v193, v54, v193
	v_mul_f32_e32 v194, v54, v194
	v_mul_f32_e32 v195, v54, v195
	ds_write_b128 v210, v[192:195] offset:4096
	v_mul_f32_e32 v196, v55, v196
	v_mul_f32_e32 v197, v55, v197
	v_mul_f32_e32 v198, v55, v198
	v_mul_f32_e32 v199, v55, v199
	ds_write_b128 v210, v[196:199] offset:5120
	v_mul_f32_e32 v200, v56, v200
	v_mul_f32_e32 v201, v56, v201
	v_mul_f32_e32 v202, v56, v202
	v_mul_f32_e32 v203, v56, v203
	ds_write_b128 v210, v[200:203] offset:6144
	v_mul_f32_e32 v204, v57, v204
	v_mul_f32_e32 v205, v57, v205
	v_mul_f32_e32 v206, v57, v206
	v_mul_f32_e32 v207, v57, v207
	ds_write_b128 v210, v[204:207] offset:7168
	s_waitcnt lgkmcnt(0)
	s_barrier
; #define GAS __attribute__((address_space(1)))
; #define LAS __attribute__((address_space(3)))
; #define LDS_WAIT() asm volatile("s_waitcnt lgkmcnt(0)" ::: "memory")
; __device__ __forceinline__ int src_col_in(int c) {
;     if (c < 5120) { const int blk = c >> 7, p = c & 127; const bool rope = blk < 16 || ((((blk - 16) >> 2) & 1) == 0); const int d = rope ? (p >> 1) + 64 * (p & 1) : p; return blk * 128 + d; }
;     if (c < OFF_Z) return c + 2096;
;     if (c < OFF_G) return c - 4048;
;     if (c < OFF_DT) return 5120 + (c - OFF_G);
;     if (c < NSRC) return c;
;     return -1;
;     const int pr = item >> 1, kb = 2 * (pr / nblk) + (item & 1), nb = pr % nblk, k0 = 64 * kb, n0 = 32 * nb;
;     const int nr = n0 + (lane & 31); const int sc = MAP == 1 ? src_col_in(nr) : nr;
;     float v[32];
; #pragma unroll
;     for (int i = 0; i < 32; ++i) v[i] = sc >= 0 ? W[(size_t)(k0 + 2 * i + (lane >> 5)) * Nsrc + sc] : 0.f;
; #pragma unroll
;     for (int i = 0; i < 32; ++i) { const int k = k0 + 2 * i + (lane >> 5); float x = v[i] * wscale; if (KS) x *= (k < ksplit ? ksA[k] : ksB[k - ksplit]); scr[(2 * i + (lane >> 5)) * 33 + (lane & 31)] = x; }
;     LDS_WAIT(); asm volatile("" ::: "memory");
;     const int c = lane & 7;
; #pragma unroll
;     for (int j = 0; j < 4; ++j) { const int n = (lane >> 3) + 8 * j; const LAS float* s = scr + (8 * c) * 33 + n;
;         const unsigned long long o = (unsigned long long)pg8::pk4_fp8(s[0 * 33], s[1 * 33], s[2 * 33], s[3 * 33]) | ((unsigned long long)pg8::pk4_fp8(s[4 * 33], s[5 * 33], s[6 * 33], s[7 * 33]) << 32);
;         *(GAS unsigned long long*)(WT + (size_t)(n0 + n) * K + k0 + 8 * c) = o; }
;     LDS_WAIT(); asm volatile("" ::: "memory");
	s_add_i32 s24, s23, 32
	s_lshl_b32 s20, s24, 7
	s_cmp_lt_u32 s24, 40
	s_cselect_b32 s21, 0, 0x830
	s_cmp_lt_u32 s24, 72
	s_cselect_b32 s21, s21, 0xfffff030
	s_add_i32 s20, s20, s21
	s_lshl_b32 s20, s20, 2
	s_add_u32 s8, s50, s20
	s_addc_u32 s9, s51, 0
	global_load_dwordx4 v[176:179], v76, s[8:9]
	s_add_u32 s8, s8, 0x16280
	s_addc_u32 s9, s9, 0
	global_load_dwordx4 v[180:183], v76, s[8:9]
	s_add_u32 s8, s8, 0x16280
	s_addc_u32 s9, s9, 0
	global_load_dwordx4 v[184:187], v76, s[8:9]
	s_add_u32 s8, s8, 0x16280
	s_addc_u32 s9, s9, 0
	global_load_dwordx4 v[188:191], v76, s[8:9]
	s_add_u32 s8, s8, 0x16280
	s_addc_u32 s9, s9, 0
	global_load_dwordx4 v[192:195], v76, s[8:9]
	s_add_u32 s8, s8, 0x16280
	s_addc_u32 s9, s9, 0
	global_load_dwordx4 v[196:199], v76, s[8:9]
	s_add_u32 s8, s8, 0x16280
	s_addc_u32 s9, s9, 0
	global_load_dwordx4 v[200:203], v76, s[8:9]
	s_add_u32 s8, s8, 0x16280
	s_addc_u32 s9, s9, 0
	global_load_dwordx4 v[204:207], v76, s[8:9]
	s_add_i32 s24, s23, 16
	s_mul_i32 s20, s24, 0x80000
	s_add_u32 s6, s52, s20
	s_addc_u32 s7, s53, 0
	s_cmp_lt_u32 s24, 16
	s_cselect_b32 s20, 1, 0
	s_sub_i32 s21, s24, 16
	s_bitcmp0_b32 s21, 2
	s_cselect_b32 s21, 1, 0
	s_cmp_lt_u32 s24, 40
	s_cselect_b32 s21, s21, 0
	s_or_b32 s20, s20, s21
	s_cmp_lg_u32 s20, 0
	s_cselect_b64 s[20:21], -1, 0
	v_cndmask_b32_e64 v91, v77, v81, s[20:21]
	v_cndmask_b32_e64 v92, v78, v82, s[20:21]
	ds_read_b32 v226, v212
	ds_read_b32 v227, v212 offset:512
	ds_read_b32 v228, v212 offset:1024
	ds_read_b32 v229, v212 offset:1536
	ds_read_b32 v230, v212 offset:2048
	ds_read_b32 v231, v212 offset:2560
	ds_read_b32 v232, v212 offset:3072
	ds_read_b32 v233, v212 offset:3584
	ds_read_b32 v234, v212 offset:4096
	ds_read_b32 v235, v212 offset:4608
	ds_read_b32 v236, v212 offset:5120
	ds_read_b32 v237, v212 offset:5632
	ds_read_b32 v238, v212 offset:6144
	ds_read_b32 v239, v212 offset:6656
	ds_read_b32 v240, v212 offset:7168
	ds_read_b32 v241, v212 offset:7680
	s_waitcnt lgkmcnt(0)
	v_max_f32_e32 v226, v226, v226
	v_max_f32_e32 v227, v227, v227
	v_max_f32_e32 v228, v228, v228
	v_max_f32_e32 v229, v229, v229
	v_max_f32_e32 v230, v230, v230
	v_max_f32_e32 v231, v231, v231
	v_max_f32_e32 v232, v232, v232
	v_max_f32_e32 v233, v233, v233
	v_max_f32_e32 v234, v234, v234
	v_max_f32_e32 v235, v235, v235
	v_max_f32_e32 v236, v236, v236
	v_max_f32_e32 v237, v237, v237
	v_max_f32_e32 v238, v238, v238
	v_max_f32_e32 v239, v239, v239
	v_max_f32_e32 v240, v240, v240
	v_max_f32_e32 v241, v241, v241
	v_med3_f32 v226, v226, s62, v95
	v_med3_f32 v227, v227, s62, v95
	v_med3_f32 v228, v228, s62, v95
	v_med3_f32 v229, v229, s62, v95
	v_med3_f32 v230, v230, s62, v95
	v_med3_f32 v231, v231, s62, v95
	v_med3_f32 v232, v232, s62, v95
	v_med3_f32 v233, v233, s62, v95
	v_med3_f32 v234, v234, s62, v95
	v_med3_f32 v235, v235, s62, v95
	v_med3_f32 v236, v236, s62, v95
	v_med3_f32 v237, v237, s62, v95
	v_med3_f32 v238, v238, s62, v95
	v_med3_f32 v239, v239, s62, v95
	v_med3_f32 v240, v240, s62, v95
	v_med3_f32 v241, v241, s62, v95
	v_mov_b32_e32 v242, 0
	v_mov_b32_e32 v243, 0
	v_mov_b32_e32 v244, 0
	v_mov_b32_e32 v245, 0
	v_cvt_pk_fp8_f32 v242, v226, v227
	v_cvt_pk_fp8_f32 v243, v230, v231
	v_cvt_pk_fp8_f32 v244, v234, v235
	v_cvt_pk_fp8_f32 v245, v238, v239
	v_cvt_pk_fp8_f32 v242, v228, v229 op_sel:[0,0,1]
	v_cvt_pk_fp8_f32 v243, v232, v233 op_sel:[0,0,1]
	v_cvt_pk_fp8_f32 v244, v236, v237 op_sel:[0,0,1]
	v_cvt_pk_fp8_f32 v245, v240, v241 op_sel:[0,0,1]
	s_nop 0
	global_store_dwordx4 v91, v[242:245], s[6:7]
	ds_read_b32 v226, v214
	ds_read_b32 v227, v214 offset:512
	ds_read_b32 v228, v214 offset:1024
	ds_read_b32 v229, v214 offset:1536
	ds_read_b32 v230, v214 offset:2048
	ds_read_b32 v231, v214 offset:2560
	ds_read_b32 v232, v214 offset:3072
	ds_read_b32 v233, v214 offset:3584
	ds_read_b32 v234, v214 offset:4096
	ds_read_b32 v235, v214 offset:4608
	ds_read_b32 v236, v214 offset:5120
	ds_read_b32 v237, v214 offset:5632
	ds_read_b32 v238, v214 offset:6144
	ds_read_b32 v239, v214 offset:6656
	ds_read_b32 v240, v214 offset:7168
	ds_read_b32 v241, v214 offset:7680
	s_waitcnt lgkmcnt(0)
	v_max_f32_e32 v226, v226, v226
	v_max_f32_e32 v227, v227, v227
	v_max_f32_e32 v228, v228, v228
	v_max_f32_e32 v229, v229, v229
	v_max_f32_e32 v230, v230, v230
	v_max_f32_e32 v231, v231, v231
	v_max_f32_e32 v232, v232, v232
	v_max_f32_e32 v233, v233, v233
	v_max_f32_e32 v234, v234, v234
	v_max_f32_e32 v235, v235, v235
	v_max_f32_e32 v236, v236, v236
	v_max_f32_e32 v237, v237, v237
	v_max_f32_e32 v238, v238, v238
	v_max_f32_e32 v239, v239, v239
	v_max_f32_e32 v240, v240, v240
	v_max_f32_e32 v241, v241, v241
	v_med3_f32 v226, v226, s62, v95
	v_med3_f32 v227, v227, s62, v95
	v_med3_f32 v228, v228, s62, v95
	v_med3_f32 v229, v229, s62, v95
	v_med3_f32 v230, v230, s62, v95
	v_med3_f32 v231, v231, s62, v95
	v_med3_f32 v232, v232, s62, v95
	v_med3_f32 v233, v233, s62, v95
	v_med3_f32 v234, v234, s62, v95
	v_med3_f32 v235, v235, s62, v95
	v_med3_f32 v236, v236, s62, v95
	v_med3_f32 v237, v237, s62, v95
	v_med3_f32 v238, v238, s62, v95
	v_med3_f32 v239, v239, s62, v95
	v_med3_f32 v240, v240, s62, v95
	v_med3_f32 v241, v241, s62, v95
	v_mov_b32_e32 v242, 0
	v_mov_b32_e32 v243, 0
	v_mov_b32_e32 v244, 0
	v_mov_b32_e32 v245, 0
	v_cvt_pk_fp8_f32 v242, v226, v227
	v_cvt_pk_fp8_f32 v243, v230, v231
	v_cvt_pk_fp8_f32 v244, v234, v235
	v_cvt_pk_fp8_f32 v245, v238, v239
	v_cvt_pk_fp8_f32 v242, v228, v229 op_sel:[0,0,1]
	v_cvt_pk_fp8_f32 v243, v232, v233 op_sel:[0,0,1]
	v_cvt_pk_fp8_f32 v244, v236, v237 op_sel:[0,0,1]
	v_cvt_pk_fp8_f32 v245, v240, v241 op_sel:[0,0,1]
	s_nop 0
	global_store_dwordx4 v92, v[242:245], s[6:7]
	s_waitcnt vmcnt(12)
	v_mul_f32_e32 v144, v50, v144
	v_mul_f32_e32 v145, v50, v145
	v_mul_f32_e32 v146, v50, v146
	v_mul_f32_e32 v147, v50, v147
	ds_write_b128 v209, v[144:147]
	v_mul_f32_e32 v148, v51, v148
	v_mul_f32_e32 v149, v51, v149
	v_mul_f32_e32 v150, v51, v150
	v_mul_f32_e32 v151, v51, v151
	ds_write_b128 v209, v[148:151] offset:1024
	v_mul_f32_e32 v152, v52, v152
	v_mul_f32_e32 v153, v52, v153
	v_mul_f32_e32 v154, v52, v154
	v_mul_f32_e32 v155, v52, v155
	ds_write_b128 v209, v[152:155] offset:2048
	v_mul_f32_e32 v156, v53, v156
	v_mul_f32_e32 v157, v53, v157
	v_mul_f32_e32 v158, v53, v158
	v_mul_f32_e32 v159, v53, v159
	ds_write_b128 v209, v[156:159] offset:3072
	v_mul_f32_e32 v160, v54, v160
	v_mul_f32_e32 v161, v54, v161
	v_mul_f32_e32 v162, v54, v162
	v_mul_f32_e32 v163, v54, v163
	ds_write_b128 v209, v[160:163] offset:4096
	v_mul_f32_e32 v164, v55, v164
	v_mul_f32_e32 v165, v55, v165
	v_mul_f32_e32 v166, v55, v166
	v_mul_f32_e32 v167, v55, v167
	ds_write_b128 v209, v[164:167] offset:5120
	v_mul_f32_e32 v168, v56, v168
	v_mul_f32_e32 v169, v56, v169
	v_mul_f32_e32 v170, v56, v170
	v_mul_f32_e32 v171, v56, v171
	ds_write_b128 v209, v[168:171] offset:6144
	v_mul_f32_e32 v172, v57, v172
	v_mul_f32_e32 v173, v57, v173
	v_mul_f32_e32 v174, v57, v174
	v_mul_f32_e32 v175, v57, v175
	ds_write_b128 v209, v[172:175] offset:7168
	s_waitcnt lgkmcnt(0)
	s_barrier
; #define GAS __attribute__((address_space(1)))
; #define LAS __attribute__((address_space(3)))
; #define LDS_WAIT() asm volatile("s_waitcnt lgkmcnt(0)" ::: "memory")
; __device__ __forceinline__ int src_col_in(int c) {
;     if (c < 5120) { const int blk = c >> 7, p = c & 127; const bool rope = blk < 16 || ((((blk - 16) >> 2) & 1) == 0); const int d = rope ? (p >> 1) + 64 * (p & 1) : p; return blk * 128 + d; }
;     if (c < OFF_Z) return c + 2096;
;     if (c < OFF_G) return c - 4048;
;     if (c < OFF_DT) return 5120 + (c - OFF_G);
;     if (c < NSRC) return c;
;     return -1;
;     const int pr = item >> 1, kb = 2 * (pr / nblk) + (item & 1), nb = pr % nblk, k0 = 64 * kb, n0 = 32 * nb;
;     const int nr = n0 + (lane & 31); const int sc = MAP == 1 ? src_col_in(nr) : nr;
;     float v[32];
; #pragma unroll
;     for (int i = 0; i < 32; ++i) v[i] = sc >= 0 ? W[(size_t)(k0 + 2 * i + (lane >> 5)) * Nsrc + sc] : 0.f;
; #pragma unroll
;     for (int i = 0; i < 32; ++i) { const int k = k0 + 2 * i + (lane >> 5); float x = v[i] * wscale; if (KS) x *= (k < ksplit ? ksA[k] : ksB[k - ksplit]); scr[(2 * i + (lane >> 5)) * 33 + (lane & 31)] = x; }
;     LDS_WAIT(); asm volatile("" ::: "memory");
;     const int c = lane & 7;
; #pragma unroll
;     for (int j = 0; j < 4; ++j) { const int n = (lane >> 3) + 8 * j; const LAS float* s = scr + (8 * c) * 33 + n;
;         const unsigned long long o = (unsigned long long)pg8::pk4_fp8(s[0 * 33], s[1 * 33], s[2 * 33], s[3 * 33]) | ((unsigned long long)pg8::pk4_fp8(s[4 * 33], s[5 * 33], s[6 * 33], s[7 * 33]) << 32);
;         *(GAS unsigned long long*)(WT + (size_t)(n0 + n) * K + k0 + 8 * c) = o; }
;     LDS_WAIT(); asm volatile("" ::: "memory");
	s_add_i32 s24, s23, 40
	s_lshl_b32 s20, s24, 7
	s_cmp_lt_u32 s24, 40
	s_cselect_b32 s21, 0, 0x830
	s_cmp_lt_u32 s24, 72
	s_cselect_b32 s21, s21, 0xfffff030
	s_add_i32 s20, s20, s21
	s_lshl_b32 s20, s20, 2
	s_add_u32 s8, s50, s20
	s_addc_u32 s9, s51, 0
	global_load_dwordx4 v[144:147], v76, s[8:9]
	s_add_u32 s8, s8, 0x16280
	s_addc_u32 s9, s9, 0
	global_load_dwordx4 v[148:151], v76, s[8:9]
	s_add_u32 s8, s8, 0x16280
	s_addc_u32 s9, s9, 0
	global_load_dwordx4 v[152:155], v76, s[8:9]
	s_add_u32 s8, s8, 0x16280
	s_addc_u32 s9, s9, 0
	global_load_dwordx4 v[156:159], v76, s[8:9]
	s_add_u32 s8, s8, 0x16280
	s_addc_u32 s9, s9, 0
	global_load_dwordx4 v[160:163], v76, s[8:9]
	s_add_u32 s8, s8, 0x16280
	s_addc_u32 s9, s9, 0
	global_load_dwordx4 v[164:167], v76, s[8:9]
	s_add_u32 s8, s8, 0x16280
	s_addc_u32 s9, s9, 0
	global_load_dwordx4 v[168:171], v76, s[8:9]
	s_add_u32 s8, s8, 0x16280
	s_addc_u32 s9, s9, 0
	global_load_dwordx4 v[172:175], v76, s[8:9]
	s_add_i32 s24, s23, 24
	s_mul_i32 s20, s24, 0x80000
	s_add_u32 s6, s52, s20
	s_addc_u32 s7, s53, 0
	s_cmp_lt_u32 s24, 16
	s_cselect_b32 s20, 1, 0
	s_sub_i32 s21, s24, 16
	s_bitcmp0_b32 s21, 2
	s_cselect_b32 s21, 1, 0
	s_cmp_lt_u32 s24, 40
	s_cselect_b32 s21, s21, 0
	s_or_b32 s20, s20, s21
	s_cmp_lg_u32 s20, 0
	s_cselect_b64 s[20:21], -1, 0
	v_cndmask_b32_e64 v91, v77, v81, s[20:21]
	v_cndmask_b32_e64 v92, v78, v82, s[20:21]
	ds_read_b32 v226, v211
	ds_read_b32 v227, v211 offset:512
	ds_read_b32 v228, v211 offset:1024
	ds_read_b32 v229, v211 offset:1536
	ds_read_b32 v230, v211 offset:2048
	ds_read_b32 v231, v211 offset:2560
	ds_read_b32 v232, v211 offset:3072
	ds_read_b32 v233, v211 offset:3584
	ds_read_b32 v234, v211 offset:4096
	ds_read_b32 v235, v211 offset:4608
	ds_read_b32 v236, v211 offset:5120
	ds_read_b32 v237, v211 offset:5632
	ds_read_b32 v238, v211 offset:6144
	ds_read_b32 v239, v211 offset:6656
	ds_read_b32 v240, v211 offset:7168
	ds_read_b32 v241, v211 offset:7680
	s_waitcnt lgkmcnt(0)
	v_max_f32_e32 v226, v226, v226
	v_max_f32_e32 v227, v227, v227
	v_max_f32_e32 v228, v228, v228
	v_max_f32_e32 v229, v229, v229
	v_max_f32_e32 v230, v230, v230
	v_max_f32_e32 v231, v231, v231
	v_max_f32_e32 v232, v232, v232
	v_max_f32_e32 v233, v233, v233
	v_max_f32_e32 v234, v234, v234
	v_max_f32_e32 v235, v235, v235
	v_max_f32_e32 v236, v236, v236
	v_max_f32_e32 v237, v237, v237
	v_max_f32_e32 v238, v238, v238
	v_max_f32_e32 v239, v239, v239
	v_max_f32_e32 v240, v240, v240
	v_max_f32_e32 v241, v241, v241
	v_med3_f32 v226, v226, s62, v95
	v_med3_f32 v227, v227, s62, v95
	v_med3_f32 v228, v228, s62, v95
	v_med3_f32 v229, v229, s62, v95
	v_med3_f32 v230, v230, s62, v95
	v_med3_f32 v231, v231, s62, v95
	v_med3_f32 v232, v232, s62, v95
	v_med3_f32 v233, v233, s62, v95
	v_med3_f32 v234, v234, s62, v95
	v_med3_f32 v235, v235, s62, v95
	v_med3_f32 v236, v236, s62, v95
	v_med3_f32 v237, v237, s62, v95
	v_med3_f32 v238, v238, s62, v95
	v_med3_f32 v239, v239, s62, v95
	v_med3_f32 v240, v240, s62, v95
	v_med3_f32 v241, v241, s62, v95
	v_mov_b32_e32 v242, 0
	v_mov_b32_e32 v243, 0
	v_mov_b32_e32 v244, 0
	v_mov_b32_e32 v245, 0
	v_cvt_pk_fp8_f32 v242, v226, v227
	v_cvt_pk_fp8_f32 v243, v230, v231
	v_cvt_pk_fp8_f32 v244, v234, v235
	v_cvt_pk_fp8_f32 v245, v238, v239
	v_cvt_pk_fp8_f32 v242, v228, v229 op_sel:[0,0,1]
	v_cvt_pk_fp8_f32 v243, v232, v233 op_sel:[0,0,1]
	v_cvt_pk_fp8_f32 v244, v236, v237 op_sel:[0,0,1]
	v_cvt_pk_fp8_f32 v245, v240, v241 op_sel:[0,0,1]
	s_nop 0
	global_store_dwordx4 v91, v[242:245], s[6:7]
	ds_read_b32 v226, v213
	ds_read_b32 v227, v213 offset:512
	ds_read_b32 v228, v213 offset:1024
	ds_read_b32 v229, v213 offset:1536
	ds_read_b32 v230, v213 offset:2048
	ds_read_b32 v231, v213 offset:2560
	ds_read_b32 v232, v213 offset:3072
	ds_read_b32 v233, v213 offset:3584
	ds_read_b32 v234, v213 offset:4096
	ds_read_b32 v235, v213 offset:4608
	ds_read_b32 v236, v213 offset:5120
	ds_read_b32 v237, v213 offset:5632
	ds_read_b32 v238, v213 offset:6144
	ds_read_b32 v239, v213 offset:6656
	ds_read_b32 v240, v213 offset:7168
	ds_read_b32 v241, v213 offset:7680
	s_waitcnt lgkmcnt(0)
	v_max_f32_e32 v226, v226, v226
	v_max_f32_e32 v227, v227, v227
	v_max_f32_e32 v228, v228, v228
	v_max_f32_e32 v229, v229, v229
	v_max_f32_e32 v230, v230, v230
	v_max_f32_e32 v231, v231, v231
	v_max_f32_e32 v232, v232, v232
	v_max_f32_e32 v233, v233, v233
	v_max_f32_e32 v234, v234, v234
	v_max_f32_e32 v235, v235, v235
	v_max_f32_e32 v236, v236, v236
	v_max_f32_e32 v237, v237, v237
	v_max_f32_e32 v238, v238, v238
	v_max_f32_e32 v239, v239, v239
	v_max_f32_e32 v240, v240, v240
	v_max_f32_e32 v241, v241, v241
	v_med3_f32 v226, v226, s62, v95
	v_med3_f32 v227, v227, s62, v95
	v_med3_f32 v228, v228, s62, v95
	v_med3_f32 v229, v229, s62, v95
	v_med3_f32 v230, v230, s62, v95
	v_med3_f32 v231, v231, s62, v95
	v_med3_f32 v232, v232, s62, v95
	v_med3_f32 v233, v233, s62, v95
	v_med3_f32 v234, v234, s62, v95
	v_med3_f32 v235, v235, s62, v95
	v_med3_f32 v236, v236, s62, v95
	v_med3_f32 v237, v237, s62, v95
	v_med3_f32 v238, v238, s62, v95
	v_med3_f32 v239, v239, s62, v95
	v_med3_f32 v240, v240, s62, v95
	v_med3_f32 v241, v241, s62, v95
	v_mov_b32_e32 v242, 0
	v_mov_b32_e32 v243, 0
	v_mov_b32_e32 v244, 0
	v_mov_b32_e32 v245, 0
	v_cvt_pk_fp8_f32 v242, v226, v227
	v_cvt_pk_fp8_f32 v243, v230, v231
	v_cvt_pk_fp8_f32 v244, v234, v235
	v_cvt_pk_fp8_f32 v245, v238, v239
	v_cvt_pk_fp8_f32 v242, v228, v229 op_sel:[0,0,1]
	v_cvt_pk_fp8_f32 v243, v232, v233 op_sel:[0,0,1]
	v_cvt_pk_fp8_f32 v244, v236, v237 op_sel:[0,0,1]
	v_cvt_pk_fp8_f32 v245, v240, v241 op_sel:[0,0,1]
	s_nop 0
	global_store_dwordx4 v92, v[242:245], s[6:7]
	s_waitcnt vmcnt(12)
	v_mul_f32_e32 v176, v50, v176
	v_mul_f32_e32 v177, v50, v177
	v_mul_f32_e32 v178, v50, v178
	v_mul_f32_e32 v179, v50, v179
	ds_write_b128 v210, v[176:179]
	v_mul_f32_e32 v180, v51, v180
	v_mul_f32_e32 v181, v51, v181
	v_mul_f32_e32 v182, v51, v182
	v_mul_f32_e32 v183, v51, v183
	ds_write_b128 v210, v[180:183] offset:1024
	v_mul_f32_e32 v184, v52, v184
	v_mul_f32_e32 v185, v52, v185
	v_mul_f32_e32 v186, v52, v186
	v_mul_f32_e32 v187, v52, v187
	ds_write_b128 v210, v[184:187] offset:2048
	v_mul_f32_e32 v188, v53, v188
	v_mul_f32_e32 v189, v53, v189
	v_mul_f32_e32 v190, v53, v190
	v_mul_f32_e32 v191, v53, v191
	ds_write_b128 v210, v[188:191] offset:3072
	v_mul_f32_e32 v192, v54, v192
	v_mul_f32_e32 v193, v54, v193
	v_mul_f32_e32 v194, v54, v194
	v_mul_f32_e32 v195, v54, v195
	ds_write_b128 v210, v[192:195] offset:4096
	v_mul_f32_e32 v196, v55, v196
	v_mul_f32_e32 v197, v55, v197
	v_mul_f32_e32 v198, v55, v198
	v_mul_f32_e32 v199, v55, v199
	ds_write_b128 v210, v[196:199] offset:5120
	v_mul_f32_e32 v200, v56, v200
	v_mul_f32_e32 v201, v56, v201
	v_mul_f32_e32 v202, v56, v202
	v_mul_f32_e32 v203, v56, v203
	ds_write_b128 v210, v[200:203] offset:6144
	v_mul_f32_e32 v204, v57, v204
	v_mul_f32_e32 v205, v57, v205
	v_mul_f32_e32 v206, v57, v206
	v_mul_f32_e32 v207, v57, v207
	ds_write_b128 v210, v[204:207] offset:7168
	s_waitcnt lgkmcnt(0)
	s_barrier
; #define GAS __attribute__((address_space(1)))
; #define LAS __attribute__((address_space(3)))
; #define LDS_WAIT() asm volatile("s_waitcnt lgkmcnt(0)" ::: "memory")
; __device__ __forceinline__ int src_col_in(int c) {
;     if (c < 5120) { const int blk = c >> 7, p = c & 127; const bool rope = blk < 16 || ((((blk - 16) >> 2) & 1) == 0); const int d = rope ? (p >> 1) + 64 * (p & 1) : p; return blk * 128 + d; }
;     if (c < OFF_Z) return c + 2096;
;     if (c < OFF_G) return c - 4048;
;     if (c < OFF_DT) return 5120 + (c - OFF_G);
;     if (c < NSRC) return c;
;     return -1;
;     const int pr = item >> 1, kb = 2 * (pr / nblk) + (item & 1), nb = pr % nblk, k0 = 64 * kb, n0 = 32 * nb;
;     const int nr = n0 + (lane & 31); const int sc = MAP == 1 ? src_col_in(nr) : nr;
;     float v[32];
; #pragma unroll
;     for (int i = 0; i < 32; ++i) v[i] = sc >= 0 ? W[(size_t)(k0 + 2 * i + (lane >> 5)) * Nsrc + sc] : 0.f;
; #pragma unroll
;     for (int i = 0; i < 32; ++i) { const int k = k0 + 2 * i + (lane >> 5); float x = v[i] * wscale; if (KS) x *= (k < ksplit ? ksA[k] : ksB[k - ksplit]); scr[(2 * i + (lane >> 5)) * 33 + (lane & 31)] = x; }
;     LDS_WAIT(); asm volatile("" ::: "memory");
;     const int c = lane & 7;
; #pragma unroll
;     for (int j = 0; j < 4; ++j) { const int n = (lane >> 3) + 8 * j; const LAS float* s = scr + (8 * c) * 33 + n;
;         const unsigned long long o = (unsigned long long)pg8::pk4_fp8(s[0 * 33], s[1 * 33], s[2 * 33], s[3 * 33]) | ((unsigned long long)pg8::pk4_fp8(s[4 * 33], s[5 * 33], s[6 * 33], s[7 * 33]) << 32);
;         *(GAS unsigned long long*)(WT + (size_t)(n0 + n) * K + k0 + 8 * c) = o; }
;     LDS_WAIT(); asm volatile("" ::: "memory");
	s_add_i32 s24, s23, 48
	s_lshl_b32 s20, s24, 7
	s_cmp_lt_u32 s24, 40
	s_cselect_b32 s21, 0, 0x830
	s_cmp_lt_u32 s24, 72
	s_cselect_b32 s21, s21, 0xfffff030
	s_add_i32 s20, s20, s21
	s_lshl_b32 s20, s20, 2
	s_add_u32 s8, s50, s20
	s_addc_u32 s9, s51, 0
	global_load_dwordx4 v[176:179], v76, s[8:9]
	s_add_u32 s8, s8, 0x16280
	s_addc_u32 s9, s9, 0
	global_load_dwordx4 v[180:183], v76, s[8:9]
	s_add_u32 s8, s8, 0x16280
	s_addc_u32 s9, s9, 0
	global_load_dwordx4 v[184:187], v76, s[8:9]
	s_add_u32 s8, s8, 0x16280
	s_addc_u32 s9, s9, 0
	global_load_dwordx4 v[188:191], v76, s[8:9]
	s_add_u32 s8, s8, 0x16280
	s_addc_u32 s9, s9, 0
	global_load_dwordx4 v[192:195], v76, s[8:9]
	s_add_u32 s8, s8, 0x16280
	s_addc_u32 s9, s9, 0
	global_load_dwordx4 v[196:199], v76, s[8:9]
	s_add_u32 s8, s8, 0x16280
	s_addc_u32 s9, s9, 0
	global_load_dwordx4 v[200:203], v76, s[8:9]
	s_add_u32 s8, s8, 0x16280
	s_addc_u32 s9, s9, 0
	global_load_dwordx4 v[204:207], v76, s[8:9]
	s_add_i32 s24, s23, 32
	s_mul_i32 s20, s24, 0x80000
	s_add_u32 s6, s52, s20
	s_addc_u32 s7, s53, 0
	s_cmp_lt_u32 s24, 16
	s_cselect_b32 s20, 1, 0
	s_sub_i32 s21, s24, 16
	s_bitcmp0_b32 s21, 2
	s_cselect_b32 s21, 1, 0
	s_cmp_lt_u32 s24, 40
	s_cselect_b32 s21, s21, 0
	s_or_b32 s20, s20, s21
	s_cmp_lg_u32 s20, 0
	s_cselect_b64 s[20:21], -1, 0
	v_cndmask_b32_e64 v91, v77, v81, s[20:21]
	v_cndmask_b32_e64 v92, v78, v82, s[20:21]
	ds_read_b32 v226, v212
	ds_read_b32 v227, v212 offset:512
	ds_read_b32 v228, v212 offset:1024
	ds_read_b32 v229, v212 offset:1536
	ds_read_b32 v230, v212 offset:2048
	ds_read_b32 v231, v212 offset:2560
	ds_read_b32 v232, v212 offset:3072
	ds_read_b32 v233, v212 offset:3584
	ds_read_b32 v234, v212 offset:4096
	ds_read_b32 v235, v212 offset:4608
	ds_read_b32 v236, v212 offset:5120
	ds_read_b32 v237, v212 offset:5632
	ds_read_b32 v238, v212 offset:6144
	ds_read_b32 v239, v212 offset:6656
	ds_read_b32 v240, v212 offset:7168
	ds_read_b32 v241, v212 offset:7680
	s_waitcnt lgkmcnt(0)
	v_max_f32_e32 v226, v226, v226
	v_max_f32_e32 v227, v227, v227
	v_max_f32_e32 v228, v228, v228
	v_max_f32_e32 v229, v229, v229
	v_max_f32_e32 v230, v230, v230
	v_max_f32_e32 v231, v231, v231
	v_max_f32_e32 v232, v232, v232
	v_max_f32_e32 v233, v233, v233
	v_max_f32_e32 v234, v234, v234
	v_max_f32_e32 v235, v235, v235
	v_max_f32_e32 v236, v236, v236
	v_max_f32_e32 v237, v237, v237
	v_max_f32_e32 v238, v238, v238
	v_max_f32_e32 v239, v239, v239
	v_max_f32_e32 v240, v240, v240
	v_max_f32_e32 v241, v241, v241
	v_med3_f32 v226, v226, s62, v95
	v_med3_f32 v227, v227, s62, v95
	v_med3_f32 v228, v228, s62, v95
	v_med3_f32 v229, v229, s62, v95
	v_med3_f32 v230, v230, s62, v95
	v_med3_f32 v231, v231, s62, v95
	v_med3_f32 v232, v232, s62, v95
	v_med3_f32 v233, v233, s62, v95
	v_med3_f32 v234, v234, s62, v95
	v_med3_f32 v235, v235, s62, v95
	v_med3_f32 v236, v236, s62, v95
	v_med3_f32 v237, v237, s62, v95
	v_med3_f32 v238, v238, s62, v95
	v_med3_f32 v239, v239, s62, v95
	v_med3_f32 v240, v240, s62, v95
	v_med3_f32 v241, v241, s62, v95
	v_mov_b32_e32 v242, 0
	v_mov_b32_e32 v243, 0
	v_mov_b32_e32 v244, 0
	v_mov_b32_e32 v245, 0
	v_cvt_pk_fp8_f32 v242, v226, v227
	v_cvt_pk_fp8_f32 v243, v230, v231
	v_cvt_pk_fp8_f32 v244, v234, v235
	v_cvt_pk_fp8_f32 v245, v238, v239
	v_cvt_pk_fp8_f32 v242, v228, v229 op_sel:[0,0,1]
	v_cvt_pk_fp8_f32 v243, v232, v233 op_sel:[0,0,1]
	v_cvt_pk_fp8_f32 v244, v236, v237 op_sel:[0,0,1]
	v_cvt_pk_fp8_f32 v245, v240, v241 op_sel:[0,0,1]
	s_nop 0
	global_store_dwordx4 v91, v[242:245], s[6:7]
	ds_read_b32 v226, v214
	ds_read_b32 v227, v214 offset:512
	ds_read_b32 v228, v214 offset:1024
	ds_read_b32 v229, v214 offset:1536
	ds_read_b32 v230, v214 offset:2048
	ds_read_b32 v231, v214 offset:2560
	ds_read_b32 v232, v214 offset:3072
	ds_read_b32 v233, v214 offset:3584
	ds_read_b32 v234, v214 offset:4096
	ds_read_b32 v235, v214 offset:4608
	ds_read_b32 v236, v214 offset:5120
	ds_read_b32 v237, v214 offset:5632
	ds_read_b32 v238, v214 offset:6144
	ds_read_b32 v239, v214 offset:6656
	ds_read_b32 v240, v214 offset:7168
	ds_read_b32 v241, v214 offset:7680
	s_waitcnt lgkmcnt(0)
	v_max_f32_e32 v226, v226, v226
	v_max_f32_e32 v227, v227, v227
	v_max_f32_e32 v228, v228, v228
	v_max_f32_e32 v229, v229, v229
	v_max_f32_e32 v230, v230, v230
	v_max_f32_e32 v231, v231, v231
	v_max_f32_e32 v232, v232, v232
	v_max_f32_e32 v233, v233, v233
	v_max_f32_e32 v234, v234, v234
	v_max_f32_e32 v235, v235, v235
	v_max_f32_e32 v236, v236, v236
	v_max_f32_e32 v237, v237, v237
	v_max_f32_e32 v238, v238, v238
	v_max_f32_e32 v239, v239, v239
	v_max_f32_e32 v240, v240, v240
	v_max_f32_e32 v241, v241, v241
	v_med3_f32 v226, v226, s62, v95
	v_med3_f32 v227, v227, s62, v95
	v_med3_f32 v228, v228, s62, v95
	v_med3_f32 v229, v229, s62, v95
	v_med3_f32 v230, v230, s62, v95
	v_med3_f32 v231, v231, s62, v95
	v_med3_f32 v232, v232, s62, v95
	v_med3_f32 v233, v233, s62, v95
	v_med3_f32 v234, v234, s62, v95
	v_med3_f32 v235, v235, s62, v95
	v_med3_f32 v236, v236, s62, v95
	v_med3_f32 v237, v237, s62, v95
	v_med3_f32 v238, v238, s62, v95
	v_med3_f32 v239, v239, s62, v95
	v_med3_f32 v240, v240, s62, v95
	v_med3_f32 v241, v241, s62, v95
	v_mov_b32_e32 v242, 0
	v_mov_b32_e32 v243, 0
	v_mov_b32_e32 v244, 0
	v_mov_b32_e32 v245, 0
	v_cvt_pk_fp8_f32 v242, v226, v227
	v_cvt_pk_fp8_f32 v243, v230, v231
	v_cvt_pk_fp8_f32 v244, v234, v235
	v_cvt_pk_fp8_f32 v245, v238, v239
	v_cvt_pk_fp8_f32 v242, v228, v229 op_sel:[0,0,1]
	v_cvt_pk_fp8_f32 v243, v232, v233 op_sel:[0,0,1]
	v_cvt_pk_fp8_f32 v244, v236, v237 op_sel:[0,0,1]
	v_cvt_pk_fp8_f32 v245, v240, v241 op_sel:[0,0,1]
	s_nop 0
	global_store_dwordx4 v92, v[242:245], s[6:7]
	s_waitcnt vmcnt(12)
	v_mul_f32_e32 v144, v50, v144
	v_mul_f32_e32 v145, v50, v145
	v_mul_f32_e32 v146, v50, v146
	v_mul_f32_e32 v147, v50, v147
	ds_write_b128 v209, v[144:147]
	v_mul_f32_e32 v148, v51, v148
	v_mul_f32_e32 v149, v51, v149
	v_mul_f32_e32 v150, v51, v150
	v_mul_f32_e32 v151, v51, v151
	ds_write_b128 v209, v[148:151] offset:1024
	v_mul_f32_e32 v152, v52, v152
	v_mul_f32_e32 v153, v52, v153
	v_mul_f32_e32 v154, v52, v154
	v_mul_f32_e32 v155, v52, v155
	ds_write_b128 v209, v[152:155] offset:2048
	v_mul_f32_e32 v156, v53, v156
	v_mul_f32_e32 v157, v53, v157
	v_mul_f32_e32 v158, v53, v158
	v_mul_f32_e32 v159, v53, v159
	ds_write_b128 v209, v[156:159] offset:3072
	v_mul_f32_e32 v160, v54, v160
	v_mul_f32_e32 v161, v54, v161
	v_mul_f32_e32 v162, v54, v162
	v_mul_f32_e32 v163, v54, v163
	ds_write_b128 v209, v[160:163] offset:4096
	v_mul_f32_e32 v164, v55, v164
	v_mul_f32_e32 v165, v55, v165
	v_mul_f32_e32 v166, v55, v166
	v_mul_f32_e32 v167, v55, v167
	ds_write_b128 v209, v[164:167] offset:5120
	v_mul_f32_e32 v168, v56, v168
	v_mul_f32_e32 v169, v56, v169
	v_mul_f32_e32 v170, v56, v170
	v_mul_f32_e32 v171, v56, v171
	ds_write_b128 v209, v[168:171] offset:6144
	v_mul_f32_e32 v172, v57, v172
	v_mul_f32_e32 v173, v57, v173
	v_mul_f32_e32 v174, v57, v174
	v_mul_f32_e32 v175, v57, v175
	ds_write_b128 v209, v[172:175] offset:7168
	s_waitcnt lgkmcnt(0)
	s_barrier
; #define GAS __attribute__((address_space(1)))
; #define LAS __attribute__((address_space(3)))
; #define LDS_WAIT() asm volatile("s_waitcnt lgkmcnt(0)" ::: "memory")
; __device__ __forceinline__ int src_col_in(int c) {
;     if (c < 5120) { const int blk = c >> 7, p = c & 127; const bool rope = blk < 16 || ((((blk - 16) >> 2) & 1) == 0); const int d = rope ? (p >> 1) + 64 * (p & 1) : p; return blk * 128 + d; }
;     if (c < OFF_Z) return c + 2096;
;     if (c < OFF_G) return c - 4048;
;     if (c < OFF_DT) return 5120 + (c - OFF_G);
;     if (c < NSRC) return c;
;     return -1;
; }
;     const int pr = item >> 1, kb = 2 * (pr / nblk) + (item & 1), nb = pr % nblk, k0 = 64 * kb, n0 = 32 * nb;
;     const int nr = n0 + (lane & 31); const int sc = MAP == 1 ? src_col_in(nr) : nr;
;     float v[32];
; #pragma unroll
;     for (int i = 0; i < 32; ++i) v[i] = sc >= 0 ? W[(size_t)(k0 + 2 * i + (lane >> 5)) * Nsrc + sc] : 0.f;
; #pragma unroll
;     for (int i = 0; i < 32; ++i) { const int k = k0 + 2 * i + (lane >> 5); float x = v[i] * wscale; if (KS) x *= (k < ksplit ? ksA[k] : ksB[k - ksplit]); scr[(2 * i + (lane >> 5)) * 33 + (lane & 31)] = x; }
;     LDS_WAIT(); asm volatile("" ::: "memory");
;     const int c = lane & 7;
; #pragma unroll
;     for (int j = 0; j < 4; ++j) { const int n = (lane >> 3) + 8 * j; const LAS float* s = scr + (8 * c) * 33 + n;
;         const unsigned long long o = (unsigned long long)pg8::pk4_fp8(s[0 * 33], s[1 * 33], s[2 * 33], s[3 * 33]) | ((unsigned long long)pg8::pk4_fp8(s[4 * 33], s[5 * 33], s[6 * 33], s[7 * 33]) << 32);
;         *(GAS unsigned long long*)(WT + (size_t)(n0 + n) * K + k0 + 8 * c) = o; }
;     LDS_WAIT(); asm volatile("" ::: "memory");
	s_add_i32 s24, s23, 56
	s_lshl_b32 s20, s24, 7
	s_cmp_lt_u32 s24, 40
	s_cselect_b32 s21, 0, 0x830
	s_cmp_lt_u32 s24, 72
	s_cselect_b32 s21, s21, 0xfffff030
	s_add_i32 s20, s20, s21
	s_lshl_b32 s20, s20, 2
	s_add_u32 s8, s50, s20
	s_addc_u32 s9, s51, 0
	global_load_dwordx4 v[144:147], v76, s[8:9]
	s_add_u32 s8, s8, 0x16280
	s_addc_u32 s9, s9, 0
	global_load_dwordx4 v[148:151], v76, s[8:9]
	s_add_u32 s8, s8, 0x16280
	s_addc_u32 s9, s9, 0
	global_load_dwordx4 v[152:155], v76, s[8:9]
	s_add_u32 s8, s8, 0x16280
	s_addc_u32 s9, s9, 0
	global_load_dwordx4 v[156:159], v76, s[8:9]
	s_add_u32 s8, s8, 0x16280
	s_addc_u32 s9, s9, 0
	global_load_dwordx4 v[160:163], v76, s[8:9]
	s_add_u32 s8, s8, 0x16280
	s_addc_u32 s9, s9, 0
	global_load_dwordx4 v[164:167], v76, s[8:9]
	s_add_u32 s8, s8, 0x16280
	s_addc_u32 s9, s9, 0
	global_load_dwordx4 v[168:171], v76, s[8:9]
	s_add_u32 s8, s8, 0x16280
	s_addc_u32 s9, s9, 0
	global_load_dwordx4 v[172:175], v76, s[8:9]
	s_add_i32 s24, s23, 40
	s_mul_i32 s20, s24, 0x80000
	s_add_u32 s6, s52, s20
	s_addc_u32 s7, s53, 0
	s_cmp_lt_u32 s24, 16
	s_cselect_b32 s20, 1, 0
	s_sub_i32 s21, s24, 16
	s_bitcmp0_b32 s21, 2
	s_cselect_b32 s21, 1, 0
	s_cmp_lt_u32 s24, 40
	s_cselect_b32 s21, s21, 0
	s_or_b32 s20, s20, s21
	s_cmp_lg_u32 s20, 0
	s_cselect_b64 s[20:21], -1, 0
	v_cndmask_b32_e64 v91, v77, v81, s[20:21]
	v_cndmask_b32_e64 v92, v78, v82, s[20:21]
	ds_read_b32 v226, v211
	ds_read_b32 v227, v211 offset:512
	ds_read_b32 v228, v211 offset:1024
	ds_read_b32 v229, v211 offset:1536
	ds_read_b32 v230, v211 offset:2048
	ds_read_b32 v231, v211 offset:2560
	ds_read_b32 v232, v211 offset:3072
	ds_read_b32 v233, v211 offset:3584
	ds_read_b32 v234, v211 offset:4096
	ds_read_b32 v235, v211 offset:4608
	ds_read_b32 v236, v211 offset:5120
	ds_read_b32 v237, v211 offset:5632
	ds_read_b32 v238, v211 offset:6144
	ds_read_b32 v239, v211 offset:6656
	ds_read_b32 v240, v211 offset:7168
	ds_read_b32 v241, v211 offset:7680
	s_waitcnt lgkmcnt(0)
	v_max_f32_e32 v226, v226, v226
	v_max_f32_e32 v227, v227, v227
	v_max_f32_e32 v228, v228, v228
	v_max_f32_e32 v229, v229, v229
	v_max_f32_e32 v230, v230, v230
	v_max_f32_e32 v231, v231, v231
	v_max_f32_e32 v232, v232, v232
	v_max_f32_e32 v233, v233, v233
	v_max_f32_e32 v234, v234, v234
	v_max_f32_e32 v235, v235, v235
	v_max_f32_e32 v236, v236, v236
	v_max_f32_e32 v237, v237, v237
	v_max_f32_e32 v238, v238, v238
	v_max_f32_e32 v239, v239, v239
	v_max_f32_e32 v240, v240, v240
	v_max_f32_e32 v241, v241, v241
	v_med3_f32 v226, v226, s62, v95
	v_med3_f32 v227, v227, s62, v95
	v_med3_f32 v228, v228, s62, v95
	v_med3_f32 v229, v229, s62, v95
	v_med3_f32 v230, v230, s62, v95
	v_med3_f32 v231, v231, s62, v95
	v_med3_f32 v232, v232, s62, v95
	v_med3_f32 v233, v233, s62, v95
	v_med3_f32 v234, v234, s62, v95
	v_med3_f32 v235, v235, s62, v95
	v_med3_f32 v236, v236, s62, v95
	v_med3_f32 v237, v237, s62, v95
	v_med3_f32 v238, v238, s62, v95
	v_med3_f32 v239, v239, s62, v95
	v_med3_f32 v240, v240, s62, v95
	v_med3_f32 v241, v241, s62, v95
	v_mov_b32_e32 v242, 0
	v_mov_b32_e32 v243, 0
	v_mov_b32_e32 v244, 0
	v_mov_b32_e32 v245, 0
	v_cvt_pk_fp8_f32 v242, v226, v227
	v_cvt_pk_fp8_f32 v243, v230, v231
	v_cvt_pk_fp8_f32 v244, v234, v235
	v_cvt_pk_fp8_f32 v245, v238, v239
	v_cvt_pk_fp8_f32 v242, v228, v229 op_sel:[0,0,1]
	v_cvt_pk_fp8_f32 v243, v232, v233 op_sel:[0,0,1]
	v_cvt_pk_fp8_f32 v244, v236, v237 op_sel:[0,0,1]
	v_cvt_pk_fp8_f32 v245, v240, v241 op_sel:[0,0,1]
	s_nop 0
	global_store_dwordx4 v91, v[242:245], s[6:7]
	ds_read_b32 v226, v213
	ds_read_b32 v227, v213 offset:512
	ds_read_b32 v228, v213 offset:1024
	ds_read_b32 v229, v213 offset:1536
	ds_read_b32 v230, v213 offset:2048
	ds_read_b32 v231, v213 offset:2560
	ds_read_b32 v232, v213 offset:3072
	ds_read_b32 v233, v213 offset:3584
	ds_read_b32 v234, v213 offset:4096
	ds_read_b32 v235, v213 offset:4608
	ds_read_b32 v236, v213 offset:5120
	ds_read_b32 v237, v213 offset:5632
	ds_read_b32 v238, v213 offset:6144
	ds_read_b32 v239, v213 offset:6656
	ds_read_b32 v240, v213 offset:7168
	ds_read_b32 v241, v213 offset:7680
	s_waitcnt lgkmcnt(0)
	v_max_f32_e32 v226, v226, v226
	v_max_f32_e32 v227, v227, v227
	v_max_f32_e32 v228, v228, v228
	v_max_f32_e32 v229, v229, v229
	v_max_f32_e32 v230, v230, v230
	v_max_f32_e32 v231, v231, v231
	v_max_f32_e32 v232, v232, v232
	v_max_f32_e32 v233, v233, v233
	v_max_f32_e32 v234, v234, v234
	v_max_f32_e32 v235, v235, v235
	v_max_f32_e32 v236, v236, v236
	v_max_f32_e32 v237, v237, v237
	v_max_f32_e32 v238, v238, v238
	v_max_f32_e32 v239, v239, v239
	v_max_f32_e32 v240, v240, v240
	v_max_f32_e32 v241, v241, v241
	v_med3_f32 v226, v226, s62, v95
	v_med3_f32 v227, v227, s62, v95
	v_med3_f32 v228, v228, s62, v95
	v_med3_f32 v229, v229, s62, v95
	v_med3_f32 v230, v230, s62, v95
	v_med3_f32 v231, v231, s62, v95
	v_med3_f32 v232, v232, s62, v95
	v_med3_f32 v233, v233, s62, v95
	v_med3_f32 v234, v234, s62, v95
	v_med3_f32 v235, v235, s62, v95
	v_med3_f32 v236, v236, s62, v95
	v_med3_f32 v237, v237, s62, v95
	v_med3_f32 v238, v238, s62, v95
	v_med3_f32 v239, v239, s62, v95
	v_med3_f32 v240, v240, s62, v95
	v_med3_f32 v241, v241, s62, v95
	v_mov_b32_e32 v242, 0
	v_mov_b32_e32 v243, 0
	v_mov_b32_e32 v244, 0
	v_mov_b32_e32 v245, 0
	v_cvt_pk_fp8_f32 v242, v226, v227
	v_cvt_pk_fp8_f32 v243, v230, v231
	v_cvt_pk_fp8_f32 v244, v234, v235
	v_cvt_pk_fp8_f32 v245, v238, v239
	v_cvt_pk_fp8_f32 v242, v228, v229 op_sel:[0,0,1]
	v_cvt_pk_fp8_f32 v243, v232, v233 op_sel:[0,0,1]
	v_cvt_pk_fp8_f32 v244, v236, v237 op_sel:[0,0,1]
	v_cvt_pk_fp8_f32 v245, v240, v241 op_sel:[0,0,1]
	s_nop 0
	global_store_dwordx4 v92, v[242:245], s[6:7]
	s_waitcnt vmcnt(12)
	v_mul_f32_e32 v176, v50, v176
	v_mul_f32_e32 v177, v50, v177
	v_mul_f32_e32 v178, v50, v178
	v_mul_f32_e32 v179, v50, v179
	ds_write_b128 v210, v[176:179]
	v_mul_f32_e32 v180, v51, v180
	v_mul_f32_e32 v181, v51, v181
	v_mul_f32_e32 v182, v51, v182
	v_mul_f32_e32 v183, v51, v183
	ds_write_b128 v210, v[180:183] offset:1024
	v_mul_f32_e32 v184, v52, v184
	v_mul_f32_e32 v185, v52, v185
	v_mul_f32_e32 v186, v52, v186
	v_mul_f32_e32 v187, v52, v187
	ds_write_b128 v210, v[184:187] offset:2048
	v_mul_f32_e32 v188, v53, v188
	v_mul_f32_e32 v189, v53, v189
	v_mul_f32_e32 v190, v53, v190
	v_mul_f32_e32 v191, v53, v191
	ds_write_b128 v210, v[188:191] offset:3072
	v_mul_f32_e32 v192, v54, v192
	v_mul_f32_e32 v193, v54, v193
	v_mul_f32_e32 v194, v54, v194
	v_mul_f32_e32 v195, v54, v195
	ds_write_b128 v210, v[192:195] offset:4096
	v_mul_f32_e32 v196, v55, v196
	v_mul_f32_e32 v197, v55, v197
	v_mul_f32_e32 v198, v55, v198
	v_mul_f32_e32 v199, v55, v199
	ds_write_b128 v210, v[196:199] offset:5120
	v_mul_f32_e32 v200, v56, v200
	v_mul_f32_e32 v201, v56, v201
	v_mul_f32_e32 v202, v56, v202
	v_mul_f32_e32 v203, v56, v203
	ds_write_b128 v210, v[200:203] offset:6144
	v_mul_f32_e32 v204, v57, v204
	v_mul_f32_e32 v205, v57, v205
	v_mul_f32_e32 v206, v57, v206
	v_mul_f32_e32 v207, v57, v207
	ds_write_b128 v210, v[204:207] offset:7168
	s_waitcnt lgkmcnt(0)
	s_barrier
; #define GAS __attribute__((address_space(1)))
; #define LAS __attribute__((address_space(3)))
; #define LDS_WAIT() asm volatile("s_waitcnt lgkmcnt(0)" ::: "memory")
; __device__ __forceinline__ int src_col_in(int c) {
;     if (c < 5120) { const int blk = c >> 7, p = c & 127; const bool rope = blk < 16 || ((((blk - 16) >> 2) & 1) == 0); const int d = rope ? (p >> 1) + 64 * (p & 1) : p; return blk * 128 + d; }
;     if (c < OFF_Z) return c + 2096;
;     if (c < OFF_G) return c - 4048;
;     if (c < OFF_DT) return 5120 + (c - OFF_G);
;     if (c < NSRC) return c;
;     return -1;
; }
;     const int pr = item >> 1, kb = 2 * (pr / nblk) + (item & 1), nb = pr % nblk, k0 = 64 * kb, n0 = 32 * nb;
;     const int nr = n0 + (lane & 31); const int sc = MAP == 1 ? src_col_in(nr) : nr;
;     float v[32];
; #pragma unroll
;     for (int i = 0; i < 32; ++i) v[i] = sc >= 0 ? W[(size_t)(k0 + 2 * i + (lane >> 5)) * Nsrc + sc] : 0.f;
; #pragma unroll
;     for (int i = 0; i < 32; ++i) { const int k = k0 + 2 * i + (lane >> 5); float x = v[i] * wscale; if (KS) x *= (k < ksplit ? ksA[k] : ksB[k - ksplit]); scr[(2 * i + (lane >> 5)) * 33 + (lane & 31)] = x; }
;     LDS_WAIT(); asm volatile("" ::: "memory");
;     const int c = lane & 7;
; #pragma unroll
;     for (int j = 0; j < 4; ++j) { const int n = (lane >> 3) + 8 * j; const LAS float* s = scr + (8 * c) * 33 + n;
;         const unsigned long long o = (unsigned long long)pg8::pk4_fp8(s[0 * 33], s[1 * 33], s[2 * 33], s[3 * 33]) | ((unsigned long long)pg8::pk4_fp8(s[4 * 33], s[5 * 33], s[6 * 33], s[7 * 33]) << 32);
;         *(GAS unsigned long long*)(WT + (size_t)(n0 + n) * K + k0 + 8 * c) = o; }
;     LDS_WAIT(); asm volatile("" ::: "memory");
	s_add_i32 s24, s23, 64
	s_lshl_b32 s20, s24, 7
	s_cmp_lt_u32 s24, 40
	s_cselect_b32 s21, 0, 0x830
	s_cmp_lt_u32 s24, 72
	s_cselect_b32 s21, s21, 0xfffff030
	s_add_i32 s20, s20, s21
	s_lshl_b32 s20, s20, 2
	s_add_u32 s8, s50, s20
	s_addc_u32 s9, s51, 0
	global_load_dwordx4 v[176:179], v76, s[8:9]
	s_add_u32 s8, s8, 0x16280
	s_addc_u32 s9, s9, 0
	global_load_dwordx4 v[180:183], v76, s[8:9]
	s_add_u32 s8, s8, 0x16280
	s_addc_u32 s9, s9, 0
	global_load_dwordx4 v[184:187], v76, s[8:9]
	s_add_u32 s8, s8, 0x16280
	s_addc_u32 s9, s9, 0
	global_load_dwordx4 v[188:191], v76, s[8:9]
	s_add_u32 s8, s8, 0x16280
	s_addc_u32 s9, s9, 0
	global_load_dwordx4 v[192:195], v76, s[8:9]
	s_add_u32 s8, s8, 0x16280
	s_addc_u32 s9, s9, 0
	global_load_dwordx4 v[196:199], v76, s[8:9]
	s_add_u32 s8, s8, 0x16280
	s_addc_u32 s9, s9, 0
	global_load_dwordx4 v[200:203], v76, s[8:9]
	s_add_u32 s8, s8, 0x16280
	s_addc_u32 s9, s9, 0
	global_load_dwordx4 v[204:207], v76, s[8:9]
	s_add_i32 s24, s23, 48
	s_mul_i32 s20, s24, 0x80000
	s_add_u32 s6, s52, s20
	s_addc_u32 s7, s53, 0
	s_cmp_lt_u32 s24, 16
	s_cselect_b32 s20, 1, 0
	s_sub_i32 s21, s24, 16
	s_bitcmp0_b32 s21, 2
	s_cselect_b32 s21, 1, 0
	s_cmp_lt_u32 s24, 40
	s_cselect_b32 s21, s21, 0
	s_or_b32 s20, s20, s21
	s_cmp_lg_u32 s20, 0
	s_cselect_b64 s[20:21], -1, 0
	v_cndmask_b32_e64 v91, v77, v81, s[20:21]
	v_cndmask_b32_e64 v92, v78, v82, s[20:21]
	ds_read_b32 v226, v212
	ds_read_b32 v227, v212 offset:512
	ds_read_b32 v228, v212 offset:1024
	ds_read_b32 v229, v212 offset:1536
	ds_read_b32 v230, v212 offset:2048
	ds_read_b32 v231, v212 offset:2560
	ds_read_b32 v232, v212 offset:3072
	ds_read_b32 v233, v212 offset:3584
	ds_read_b32 v234, v212 offset:4096
	ds_read_b32 v235, v212 offset:4608
	ds_read_b32 v236, v212 offset:5120
	ds_read_b32 v237, v212 offset:5632
	ds_read_b32 v238, v212 offset:6144
	ds_read_b32 v239, v212 offset:6656
	ds_read_b32 v240, v212 offset:7168
	ds_read_b32 v241, v212 offset:7680
	s_waitcnt lgkmcnt(0)
	v_max_f32_e32 v226, v226, v226
	v_max_f32_e32 v227, v227, v227
	v_max_f32_e32 v228, v228, v228
	v_max_f32_e32 v229, v229, v229
	v_max_f32_e32 v230, v230, v230
	v_max_f32_e32 v231, v231, v231
	v_max_f32_e32 v232, v232, v232
	v_max_f32_e32 v233, v233, v233
	v_max_f32_e32 v234, v234, v234
	v_max_f32_e32 v235, v235, v235
	v_max_f32_e32 v236, v236, v236
	v_max_f32_e32 v237, v237, v237
	v_max_f32_e32 v238, v238, v238
	v_max_f32_e32 v239, v239, v239
	v_max_f32_e32 v240, v240, v240
	v_max_f32_e32 v241, v241, v241
	v_med3_f32 v226, v226, s62, v95
	v_med3_f32 v227, v227, s62, v95
	v_med3_f32 v228, v228, s62, v95
	v_med3_f32 v229, v229, s62, v95
	v_med3_f32 v230, v230, s62, v95
	v_med3_f32 v231, v231, s62, v95
	v_med3_f32 v232, v232, s62, v95
	v_med3_f32 v233, v233, s62, v95
	v_med3_f32 v234, v234, s62, v95
	v_med3_f32 v235, v235, s62, v95
	v_med3_f32 v236, v236, s62, v95
	v_med3_f32 v237, v237, s62, v95
	v_med3_f32 v238, v238, s62, v95
	v_med3_f32 v239, v239, s62, v95
	v_med3_f32 v240, v240, s62, v95
	v_med3_f32 v241, v241, s62, v95
	v_mov_b32_e32 v242, 0
	v_mov_b32_e32 v243, 0
	v_mov_b32_e32 v244, 0
	v_mov_b32_e32 v245, 0
	v_cvt_pk_fp8_f32 v242, v226, v227
	v_cvt_pk_fp8_f32 v243, v230, v231
	v_cvt_pk_fp8_f32 v244, v234, v235
	v_cvt_pk_fp8_f32 v245, v238, v239
	v_cvt_pk_fp8_f32 v242, v228, v229 op_sel:[0,0,1]
	v_cvt_pk_fp8_f32 v243, v232, v233 op_sel:[0,0,1]
	v_cvt_pk_fp8_f32 v244, v236, v237 op_sel:[0,0,1]
	v_cvt_pk_fp8_f32 v245, v240, v241 op_sel:[0,0,1]
	s_nop 0
	global_store_dwordx4 v91, v[242:245], s[6:7]
	ds_read_b32 v226, v214
	ds_read_b32 v227, v214 offset:512
	ds_read_b32 v228, v214 offset:1024
	ds_read_b32 v229, v214 offset:1536
	ds_read_b32 v230, v214 offset:2048
	ds_read_b32 v231, v214 offset:2560
	ds_read_b32 v232, v214 offset:3072
	ds_read_b32 v233, v214 offset:3584
	ds_read_b32 v234, v214 offset:4096
	ds_read_b32 v235, v214 offset:4608
	ds_read_b32 v236, v214 offset:5120
	ds_read_b32 v237, v214 offset:5632
	ds_read_b32 v238, v214 offset:6144
	ds_read_b32 v239, v214 offset:6656
	ds_read_b32 v240, v214 offset:7168
	ds_read_b32 v241, v214 offset:7680
	s_waitcnt lgkmcnt(0)
	v_max_f32_e32 v226, v226, v226
	v_max_f32_e32 v227, v227, v227
	v_max_f32_e32 v228, v228, v228
	v_max_f32_e32 v229, v229, v229
	v_max_f32_e32 v230, v230, v230
	v_max_f32_e32 v231, v231, v231
	v_max_f32_e32 v232, v232, v232
	v_max_f32_e32 v233, v233, v233
	v_max_f32_e32 v234, v234, v234
	v_max_f32_e32 v235, v235, v235
	v_max_f32_e32 v236, v236, v236
	v_max_f32_e32 v237, v237, v237
	v_max_f32_e32 v238, v238, v238
	v_max_f32_e32 v239, v239, v239
	v_max_f32_e32 v240, v240, v240
	v_max_f32_e32 v241, v241, v241
	v_med3_f32 v226, v226, s62, v95
	v_med3_f32 v227, v227, s62, v95
	v_med3_f32 v228, v228, s62, v95
	v_med3_f32 v229, v229, s62, v95
	v_med3_f32 v230, v230, s62, v95
	v_med3_f32 v231, v231, s62, v95
	v_med3_f32 v232, v232, s62, v95
	v_med3_f32 v233, v233, s62, v95
	v_med3_f32 v234, v234, s62, v95
	v_med3_f32 v235, v235, s62, v95
	v_med3_f32 v236, v236, s62, v95
	v_med3_f32 v237, v237, s62, v95
	v_med3_f32 v238, v238, s62, v95
	v_med3_f32 v239, v239, s62, v95
	v_med3_f32 v240, v240, s62, v95
	v_med3_f32 v241, v241, s62, v95
	v_mov_b32_e32 v242, 0
	v_mov_b32_e32 v243, 0
	v_mov_b32_e32 v244, 0
	v_mov_b32_e32 v245, 0
	v_cvt_pk_fp8_f32 v242, v226, v227
	v_cvt_pk_fp8_f32 v243, v230, v231
	v_cvt_pk_fp8_f32 v244, v234, v235
	v_cvt_pk_fp8_f32 v245, v238, v239
	v_cvt_pk_fp8_f32 v242, v228, v229 op_sel:[0,0,1]
	v_cvt_pk_fp8_f32 v243, v232, v233 op_sel:[0,0,1]
	v_cvt_pk_fp8_f32 v244, v236, v237 op_sel:[0,0,1]
	v_cvt_pk_fp8_f32 v245, v240, v241 op_sel:[0,0,1]
	s_nop 0
	global_store_dwordx4 v92, v[242:245], s[6:7]
	s_waitcnt vmcnt(12)
	v_mul_f32_e32 v144, v50, v144
	v_mul_f32_e32 v145, v50, v145
	v_mul_f32_e32 v146, v50, v146
	v_mul_f32_e32 v147, v50, v147
	ds_write_b128 v209, v[144:147]
	v_mul_f32_e32 v148, v51, v148
	v_mul_f32_e32 v149, v51, v149
	v_mul_f32_e32 v150, v51, v150
	v_mul_f32_e32 v151, v51, v151
	ds_write_b128 v209, v[148:151] offset:1024
	v_mul_f32_e32 v152, v52, v152
	v_mul_f32_e32 v153, v52, v153
	v_mul_f32_e32 v154, v52, v154
	v_mul_f32_e32 v155, v52, v155
	ds_write_b128 v209, v[152:155] offset:2048
	v_mul_f32_e32 v156, v53, v156
	v_mul_f32_e32 v157, v53, v157
	v_mul_f32_e32 v158, v53, v158
	v_mul_f32_e32 v159, v53, v159
	ds_write_b128 v209, v[156:159] offset:3072
	v_mul_f32_e32 v160, v54, v160
	v_mul_f32_e32 v161, v54, v161
	v_mul_f32_e32 v162, v54, v162
	v_mul_f32_e32 v163, v54, v163
	ds_write_b128 v209, v[160:163] offset:4096
	v_mul_f32_e32 v164, v55, v164
	v_mul_f32_e32 v165, v55, v165
	v_mul_f32_e32 v166, v55, v166
	v_mul_f32_e32 v167, v55, v167
	ds_write_b128 v209, v[164:167] offset:5120
	v_mul_f32_e32 v168, v56, v168
	v_mul_f32_e32 v169, v56, v169
	v_mul_f32_e32 v170, v56, v170
	v_mul_f32_e32 v171, v56, v171
	ds_write_b128 v209, v[168:171] offset:6144
	v_mul_f32_e32 v172, v57, v172
	v_mul_f32_e32 v173, v57, v173
	v_mul_f32_e32 v174, v57, v174
	v_mul_f32_e32 v175, v57, v175
	ds_write_b128 v209, v[172:175] offset:7168
	s_waitcnt lgkmcnt(0)
	s_barrier
; #define GAS __attribute__((address_space(1)))
; #define LAS __attribute__((address_space(3)))
; #define LDS_WAIT() asm volatile("s_waitcnt lgkmcnt(0)" ::: "memory")
; __device__ __forceinline__ int src_col_in(int c) {
;     if (c < 5120) { const int blk = c >> 7, p = c & 127; const bool rope = blk < 16 || ((((blk - 16) >> 2) & 1) == 0); const int d = rope ? (p >> 1) + 64 * (p & 1) : p; return blk * 128 + d; }
;     if (c < OFF_Z) return c + 2096;
;     if (c < OFF_G) return c - 4048;
;     if (c < OFF_DT) return 5120 + (c - OFF_G);
;     if (c < NSRC) return c;
;     return -1;
; }
;     const int pr = item >> 1, kb = 2 * (pr / nblk) + (item & 1), nb = pr % nblk, k0 = 64 * kb, n0 = 32 * nb;
;     const int nr = n0 + (lane & 31); const int sc = MAP == 1 ? src_col_in(nr) : nr;
;     float v[32];
; #pragma unroll
;     for (int i = 0; i < 32; ++i) v[i] = sc >= 0 ? W[(size_t)(k0 + 2 * i + (lane >> 5)) * Nsrc + sc] : 0.f;
; #pragma unroll
;     for (int i = 0; i < 32; ++i) { const int k = k0 + 2 * i + (lane >> 5); float x = v[i] * wscale; if (KS) x *= (k < ksplit ? ksA[k] : ksB[k - ksplit]); scr[(2 * i + (lane >> 5)) * 33 + (lane & 31)] = x; }
;     LDS_WAIT(); asm volatile("" ::: "memory");
;     const int c = lane & 7;
; #pragma unroll
;     for (int j = 0; j < 4; ++j) { const int n = (lane >> 3) + 8 * j; const LAS float* s = scr + (8 * c) * 33 + n;
;         const unsigned long long o = (unsigned long long)pg8::pk4_fp8(s[0 * 33], s[1 * 33], s[2 * 33], s[3 * 33]) | ((unsigned long long)pg8::pk4_fp8(s[4 * 33], s[5 * 33], s[6 * 33], s[7 * 33]) << 32);
;         *(GAS unsigned long long*)(WT + (size_t)(n0 + n) * K + k0 + 8 * c) = o; }
;     LDS_WAIT(); asm volatile("" ::: "memory");
	s_add_i32 s24, s23, 72
	s_lshl_b32 s20, s24, 7
	s_cmp_lt_u32 s24, 40
	s_cselect_b32 s21, 0, 0x830
	s_cmp_lt_u32 s24, 72
	s_cselect_b32 s21, s21, 0xfffff030
	s_add_i32 s20, s20, s21
	s_lshl_b32 s20, s20, 2
	s_add_u32 s8, s50, s20
	s_addc_u32 s9, s51, 0
	global_load_dwordx4 v[144:147], v76, s[8:9]
	s_add_u32 s8, s8, 0x16280
	s_addc_u32 s9, s9, 0
	global_load_dwordx4 v[148:151], v76, s[8:9]
	s_add_u32 s8, s8, 0x16280
	s_addc_u32 s9, s9, 0
	global_load_dwordx4 v[152:155], v76, s[8:9]
	s_add_u32 s8, s8, 0x16280
	s_addc_u32 s9, s9, 0
	global_load_dwordx4 v[156:159], v76, s[8:9]
	s_add_u32 s8, s8, 0x16280
	s_addc_u32 s9, s9, 0
	global_load_dwordx4 v[160:163], v76, s[8:9]
	s_add_u32 s8, s8, 0x16280
	s_addc_u32 s9, s9, 0
	global_load_dwordx4 v[164:167], v76, s[8:9]
	s_add_u32 s8, s8, 0x16280
	s_addc_u32 s9, s9, 0
	global_load_dwordx4 v[168:171], v76, s[8:9]
	s_add_u32 s8, s8, 0x16280
	s_addc_u32 s9, s9, 0
	global_load_dwordx4 v[172:175], v76, s[8:9]
	s_add_i32 s24, s23, 56
	s_mul_i32 s20, s24, 0x80000
	s_add_u32 s6, s52, s20
	s_addc_u32 s7, s53, 0
	s_cmp_lt_u32 s24, 16
	s_cselect_b32 s20, 1, 0
	s_sub_i32 s21, s24, 16
	s_bitcmp0_b32 s21, 2
	s_cselect_b32 s21, 1, 0
	s_cmp_lt_u32 s24, 40
	s_cselect_b32 s21, s21, 0
	s_or_b32 s20, s20, s21
	s_cmp_lg_u32 s20, 0
	s_cselect_b64 s[20:21], -1, 0
	v_cndmask_b32_e64 v91, v77, v81, s[20:21]
	v_cndmask_b32_e64 v92, v78, v82, s[20:21]
	ds_read_b32 v226, v211
	ds_read_b32 v227, v211 offset:512
	ds_read_b32 v228, v211 offset:1024
	ds_read_b32 v229, v211 offset:1536
	ds_read_b32 v230, v211 offset:2048
	ds_read_b32 v231, v211 offset:2560
	ds_read_b32 v232, v211 offset:3072
	ds_read_b32 v233, v211 offset:3584
	ds_read_b32 v234, v211 offset:4096
	ds_read_b32 v235, v211 offset:4608
	ds_read_b32 v236, v211 offset:5120
	ds_read_b32 v237, v211 offset:5632
	ds_read_b32 v238, v211 offset:6144
	ds_read_b32 v239, v211 offset:6656
	ds_read_b32 v240, v211 offset:7168
	ds_read_b32 v241, v211 offset:7680
	s_waitcnt lgkmcnt(0)
	v_max_f32_e32 v226, v226, v226
	v_max_f32_e32 v227, v227, v227
	v_max_f32_e32 v228, v228, v228
	v_max_f32_e32 v229, v229, v229
	v_max_f32_e32 v230, v230, v230
	v_max_f32_e32 v231, v231, v231
	v_max_f32_e32 v232, v232, v232
	v_max_f32_e32 v233, v233, v233
	v_max_f32_e32 v234, v234, v234
	v_max_f32_e32 v235, v235, v235
	v_max_f32_e32 v236, v236, v236
	v_max_f32_e32 v237, v237, v237
	v_max_f32_e32 v238, v238, v238
	v_max_f32_e32 v239, v239, v239
	v_max_f32_e32 v240, v240, v240
	v_max_f32_e32 v241, v241, v241
	v_med3_f32 v226, v226, s62, v95
	v_med3_f32 v227, v227, s62, v95
	v_med3_f32 v228, v228, s62, v95
	v_med3_f32 v229, v229, s62, v95
	v_med3_f32 v230, v230, s62, v95
	v_med3_f32 v231, v231, s62, v95
	v_med3_f32 v232, v232, s62, v95
	v_med3_f32 v233, v233, s62, v95
	v_med3_f32 v234, v234, s62, v95
	v_med3_f32 v235, v235, s62, v95
	v_med3_f32 v236, v236, s62, v95
	v_med3_f32 v237, v237, s62, v95
	v_med3_f32 v238, v238, s62, v95
	v_med3_f32 v239, v239, s62, v95
	v_med3_f32 v240, v240, s62, v95
	v_med3_f32 v241, v241, s62, v95
	v_mov_b32_e32 v242, 0
	v_mov_b32_e32 v243, 0
	v_mov_b32_e32 v244, 0
	v_mov_b32_e32 v245, 0
	v_cvt_pk_fp8_f32 v242, v226, v227
	v_cvt_pk_fp8_f32 v243, v230, v231
	v_cvt_pk_fp8_f32 v244, v234, v235
	v_cvt_pk_fp8_f32 v245, v238, v239
	v_cvt_pk_fp8_f32 v242, v228, v229 op_sel:[0,0,1]
	v_cvt_pk_fp8_f32 v243, v232, v233 op_sel:[0,0,1]
	v_cvt_pk_fp8_f32 v244, v236, v237 op_sel:[0,0,1]
	v_cvt_pk_fp8_f32 v245, v240, v241 op_sel:[0,0,1]
	s_nop 0
	global_store_dwordx4 v91, v[242:245], s[6:7]
	ds_read_b32 v226, v213
	ds_read_b32 v227, v213 offset:512
	ds_read_b32 v228, v213 offset:1024
	ds_read_b32 v229, v213 offset:1536
	ds_read_b32 v230, v213 offset:2048
	ds_read_b32 v231, v213 offset:2560
	ds_read_b32 v232, v213 offset:3072
	ds_read_b32 v233, v213 offset:3584
	ds_read_b32 v234, v213 offset:4096
	ds_read_b32 v235, v213 offset:4608
	ds_read_b32 v236, v213 offset:5120
	ds_read_b32 v237, v213 offset:5632
	ds_read_b32 v238, v213 offset:6144
	ds_read_b32 v239, v213 offset:6656
	ds_read_b32 v240, v213 offset:7168
	ds_read_b32 v241, v213 offset:7680
	s_waitcnt lgkmcnt(0)
	v_max_f32_e32 v226, v226, v226
	v_max_f32_e32 v227, v227, v227
	v_max_f32_e32 v228, v228, v228
	v_max_f32_e32 v229, v229, v229
	v_max_f32_e32 v230, v230, v230
	v_max_f32_e32 v231, v231, v231
	v_max_f32_e32 v232, v232, v232
	v_max_f32_e32 v233, v233, v233
	v_max_f32_e32 v234, v234, v234
	v_max_f32_e32 v235, v235, v235
	v_max_f32_e32 v236, v236, v236
	v_max_f32_e32 v237, v237, v237
	v_max_f32_e32 v238, v238, v238
	v_max_f32_e32 v239, v239, v239
	v_max_f32_e32 v240, v240, v240
	v_max_f32_e32 v241, v241, v241
	v_med3_f32 v226, v226, s62, v95
	v_med3_f32 v227, v227, s62, v95
	v_med3_f32 v228, v228, s62, v95
	v_med3_f32 v229, v229, s62, v95
	v_med3_f32 v230, v230, s62, v95
	v_med3_f32 v231, v231, s62, v95
	v_med3_f32 v232, v232, s62, v95
	v_med3_f32 v233, v233, s62, v95
	v_med3_f32 v234, v234, s62, v95
	v_med3_f32 v235, v235, s62, v95
	v_med3_f32 v236, v236, s62, v95
	v_med3_f32 v237, v237, s62, v95
	v_med3_f32 v238, v238, s62, v95
	v_med3_f32 v239, v239, s62, v95
	v_med3_f32 v240, v240, s62, v95
	v_med3_f32 v241, v241, s62, v95
	v_mov_b32_e32 v242, 0
	v_mov_b32_e32 v243, 0
	v_mov_b32_e32 v244, 0
	v_mov_b32_e32 v245, 0
	v_cvt_pk_fp8_f32 v242, v226, v227
	v_cvt_pk_fp8_f32 v243, v230, v231
	v_cvt_pk_fp8_f32 v244, v234, v235
	v_cvt_pk_fp8_f32 v245, v238, v239
	v_cvt_pk_fp8_f32 v242, v228, v229 op_sel:[0,0,1]
	v_cvt_pk_fp8_f32 v243, v232, v233 op_sel:[0,0,1]
	v_cvt_pk_fp8_f32 v244, v236, v237 op_sel:[0,0,1]
	v_cvt_pk_fp8_f32 v245, v240, v241 op_sel:[0,0,1]
	s_nop 0
	global_store_dwordx4 v92, v[242:245], s[6:7]
	s_waitcnt vmcnt(12)
	v_mul_f32_e32 v176, v50, v176
	v_mul_f32_e32 v177, v50, v177
	v_mul_f32_e32 v178, v50, v178
	v_mul_f32_e32 v179, v50, v179
	ds_write_b128 v210, v[176:179]
	v_mul_f32_e32 v180, v51, v180
	v_mul_f32_e32 v181, v51, v181
	v_mul_f32_e32 v182, v51, v182
	v_mul_f32_e32 v183, v51, v183
	ds_write_b128 v210, v[180:183] offset:1024
	v_mul_f32_e32 v184, v52, v184
	v_mul_f32_e32 v185, v52, v185
	v_mul_f32_e32 v186, v52, v186
	v_mul_f32_e32 v187, v52, v187
	ds_write_b128 v210, v[184:187] offset:2048
	v_mul_f32_e32 v188, v53, v188
	v_mul_f32_e32 v189, v53, v189
	v_mul_f32_e32 v190, v53, v190
	v_mul_f32_e32 v191, v53, v191
	ds_write_b128 v210, v[188:191] offset:3072
	v_mul_f32_e32 v192, v54, v192
	v_mul_f32_e32 v193, v54, v193
	v_mul_f32_e32 v194, v54, v194
	v_mul_f32_e32 v195, v54, v195
	ds_write_b128 v210, v[192:195] offset:4096
	v_mul_f32_e32 v196, v55, v196
	v_mul_f32_e32 v197, v55, v197
	v_mul_f32_e32 v198, v55, v198
	v_mul_f32_e32 v199, v55, v199
	ds_write_b128 v210, v[196:199] offset:5120
	v_mul_f32_e32 v200, v56, v200
	v_mul_f32_e32 v201, v56, v201
	v_mul_f32_e32 v202, v56, v202
	v_mul_f32_e32 v203, v56, v203
	ds_write_b128 v210, v[200:203] offset:6144
	v_mul_f32_e32 v204, v57, v204
	v_mul_f32_e32 v205, v57, v205
	v_mul_f32_e32 v206, v57, v206
	v_mul_f32_e32 v207, v57, v207
	ds_write_b128 v210, v[204:207] offset:7168
	s_waitcnt lgkmcnt(0)
	s_barrier
; #define GAS __attribute__((address_space(1)))
; #define LAS __attribute__((address_space(3)))
; #define LDS_WAIT() asm volatile("s_waitcnt lgkmcnt(0)" ::: "memory")
; __device__ __forceinline__ int src_col_in(int c) {
;     if (c < 5120) { const int blk = c >> 7, p = c & 127; const bool rope = blk < 16 || ((((blk - 16) >> 2) & 1) == 0); const int d = rope ? (p >> 1) + 64 * (p & 1) : p; return blk * 128 + d; }
;     if (c < OFF_Z) return c + 2096;
;     if (c < OFF_G) return c - 4048;
;     if (c < OFF_DT) return 5120 + (c - OFF_G);
;     if (c < NSRC) return c;
;     return -1;
; }
;     const int pr = item >> 1, kb = 2 * (pr / nblk) + (item & 1), nb = pr % nblk, k0 = 64 * kb, n0 = 32 * nb;
;     const int nr = n0 + (lane & 31); const int sc = MAP == 1 ? src_col_in(nr) : nr;
;     float v[32];
; #pragma unroll
;     for (int i = 0; i < 32; ++i) v[i] = sc >= 0 ? W[(size_t)(k0 + 2 * i + (lane >> 5)) * Nsrc + sc] : 0.f;
; #pragma unroll
;     for (int i = 0; i < 32; ++i) { const int k = k0 + 2 * i + (lane >> 5); float x = v[i] * wscale; if (KS) x *= (k < ksplit ? ksA[k] : ksB[k - ksplit]); scr[(2 * i + (lane >> 5)) * 33 + (lane & 31)] = x; }
;     LDS_WAIT(); asm volatile("" ::: "memory");
;     const int c = lane & 7;
; #pragma unroll
;     for (int j = 0; j < 4; ++j) { const int n = (lane >> 3) + 8 * j; const LAS float* s = scr + (8 * c) * 33 + n;
;         const unsigned long long o = (unsigned long long)pg8::pk4_fp8(s[0 * 33], s[1 * 33], s[2 * 33], s[3 * 33]) | ((unsigned long long)pg8::pk4_fp8(s[4 * 33], s[5 * 33], s[6 * 33], s[7 * 33]) << 32);
;         *(GAS unsigned long long*)(WT + (size_t)(n0 + n) * K + k0 + 8 * c) = o; }
;     LDS_WAIT(); asm volatile("" ::: "memory");
	s_add_i32 s24, s23, 80
	s_lshl_b32 s20, s24, 7
	s_cmp_lt_u32 s24, 40
	s_cselect_b32 s21, 0, 0x830
	s_cmp_lt_u32 s24, 72
	s_cselect_b32 s21, s21, 0xfffff030
	s_add_i32 s20, s20, s21
	s_lshl_b32 s20, s20, 2
	s_add_u32 s8, s50, s20
	s_addc_u32 s9, s51, 0
	global_load_dwordx4 v[176:179], v76, s[8:9]
	s_add_u32 s8, s8, 0x16280
	s_addc_u32 s9, s9, 0
	global_load_dwordx4 v[180:183], v76, s[8:9]
	s_add_u32 s8, s8, 0x16280
	s_addc_u32 s9, s9, 0
	global_load_dwordx4 v[184:187], v76, s[8:9]
	s_add_u32 s8, s8, 0x16280
	s_addc_u32 s9, s9, 0
	global_load_dwordx4 v[188:191], v76, s[8:9]
	s_add_u32 s8, s8, 0x16280
	s_addc_u32 s9, s9, 0
	global_load_dwordx4 v[192:195], v76, s[8:9]
	s_add_u32 s8, s8, 0x16280
	s_addc_u32 s9, s9, 0
	global_load_dwordx4 v[196:199], v76, s[8:9]
	s_add_u32 s8, s8, 0x16280
	s_addc_u32 s9, s9, 0
	global_load_dwordx4 v[200:203], v76, s[8:9]
	s_add_u32 s8, s8, 0x16280
	s_addc_u32 s9, s9, 0
	global_load_dwordx4 v[204:207], v76, s[8:9]
	s_add_i32 s24, s23, 64
	s_mul_i32 s20, s24, 0x80000
	s_add_u32 s6, s52, s20
	s_addc_u32 s7, s53, 0
	s_cmp_lt_u32 s24, 16
	s_cselect_b32 s20, 1, 0
	s_sub_i32 s21, s24, 16
	s_bitcmp0_b32 s21, 2
	s_cselect_b32 s21, 1, 0
	s_cmp_lt_u32 s24, 40
	s_cselect_b32 s21, s21, 0
	s_or_b32 s20, s20, s21
	s_cmp_lg_u32 s20, 0
	s_cselect_b64 s[20:21], -1, 0
	v_cndmask_b32_e64 v91, v77, v81, s[20:21]
	v_cndmask_b32_e64 v92, v78, v82, s[20:21]
	ds_read_b32 v226, v212
	ds_read_b32 v227, v212 offset:512
	ds_read_b32 v228, v212 offset:1024
	ds_read_b32 v229, v212 offset:1536
	ds_read_b32 v230, v212 offset:2048
	ds_read_b32 v231, v212 offset:2560
	ds_read_b32 v232, v212 offset:3072
	ds_read_b32 v233, v212 offset:3584
	ds_read_b32 v234, v212 offset:4096
	ds_read_b32 v235, v212 offset:4608
	ds_read_b32 v236, v212 offset:5120
	ds_read_b32 v237, v212 offset:5632
	ds_read_b32 v238, v212 offset:6144
	ds_read_b32 v239, v212 offset:6656
	ds_read_b32 v240, v212 offset:7168
	ds_read_b32 v241, v212 offset:7680
	s_waitcnt lgkmcnt(0)
	v_max_f32_e32 v226, v226, v226
	v_max_f32_e32 v227, v227, v227
	v_max_f32_e32 v228, v228, v228
	v_max_f32_e32 v229, v229, v229
	v_max_f32_e32 v230, v230, v230
	v_max_f32_e32 v231, v231, v231
	v_max_f32_e32 v232, v232, v232
	v_max_f32_e32 v233, v233, v233
	v_max_f32_e32 v234, v234, v234
	v_max_f32_e32 v235, v235, v235
	v_max_f32_e32 v236, v236, v236
	v_max_f32_e32 v237, v237, v237
	v_max_f32_e32 v238, v238, v238
	v_max_f32_e32 v239, v239, v239
	v_max_f32_e32 v240, v240, v240
	v_max_f32_e32 v241, v241, v241
	v_med3_f32 v226, v226, s62, v95
	v_med3_f32 v227, v227, s62, v95
	v_med3_f32 v228, v228, s62, v95
	v_med3_f32 v229, v229, s62, v95
	v_med3_f32 v230, v230, s62, v95
	v_med3_f32 v231, v231, s62, v95
	v_med3_f32 v232, v232, s62, v95
	v_med3_f32 v233, v233, s62, v95
	v_med3_f32 v234, v234, s62, v95
	v_med3_f32 v235, v235, s62, v95
	v_med3_f32 v236, v236, s62, v95
	v_med3_f32 v237, v237, s62, v95
	v_med3_f32 v238, v238, s62, v95
	v_med3_f32 v239, v239, s62, v95
	v_med3_f32 v240, v240, s62, v95
	v_med3_f32 v241, v241, s62, v95
	v_mov_b32_e32 v242, 0
	v_mov_b32_e32 v243, 0
	v_mov_b32_e32 v244, 0
	v_mov_b32_e32 v245, 0
	v_cvt_pk_fp8_f32 v242, v226, v227
	v_cvt_pk_fp8_f32 v243, v230, v231
	v_cvt_pk_fp8_f32 v244, v234, v235
	v_cvt_pk_fp8_f32 v245, v238, v239
	v_cvt_pk_fp8_f32 v242, v228, v229 op_sel:[0,0,1]
	v_cvt_pk_fp8_f32 v243, v232, v233 op_sel:[0,0,1]
	v_cvt_pk_fp8_f32 v244, v236, v237 op_sel:[0,0,1]
	v_cvt_pk_fp8_f32 v245, v240, v241 op_sel:[0,0,1]
	s_nop 0
	global_store_dwordx4 v91, v[242:245], s[6:7]
	ds_read_b32 v226, v214
	ds_read_b32 v227, v214 offset:512
	ds_read_b32 v228, v214 offset:1024
	ds_read_b32 v229, v214 offset:1536
	ds_read_b32 v230, v214 offset:2048
	ds_read_b32 v231, v214 offset:2560
	ds_read_b32 v232, v214 offset:3072
	ds_read_b32 v233, v214 offset:3584
	ds_read_b32 v234, v214 offset:4096
	ds_read_b32 v235, v214 offset:4608
	ds_read_b32 v236, v214 offset:5120
	ds_read_b32 v237, v214 offset:5632
	ds_read_b32 v238, v214 offset:6144
	ds_read_b32 v239, v214 offset:6656
	ds_read_b32 v240, v214 offset:7168
	ds_read_b32 v241, v214 offset:7680
	s_waitcnt lgkmcnt(0)
	v_max_f32_e32 v226, v226, v226
	v_max_f32_e32 v227, v227, v227
	v_max_f32_e32 v228, v228, v228
	v_max_f32_e32 v229, v229, v229
	v_max_f32_e32 v230, v230, v230
	v_max_f32_e32 v231, v231, v231
	v_max_f32_e32 v232, v232, v232
	v_max_f32_e32 v233, v233, v233
	v_max_f32_e32 v234, v234, v234
	v_max_f32_e32 v235, v235, v235
	v_max_f32_e32 v236, v236, v236
	v_max_f32_e32 v237, v237, v237
	v_max_f32_e32 v238, v238, v238
	v_max_f32_e32 v239, v239, v239
	v_max_f32_e32 v240, v240, v240
	v_max_f32_e32 v241, v241, v241
	v_med3_f32 v226, v226, s62, v95
	v_med3_f32 v227, v227, s62, v95
	v_med3_f32 v228, v228, s62, v95
	v_med3_f32 v229, v229, s62, v95
	v_med3_f32 v230, v230, s62, v95
	v_med3_f32 v231, v231, s62, v95
	v_med3_f32 v232, v232, s62, v95
	v_med3_f32 v233, v233, s62, v95
	v_med3_f32 v234, v234, s62, v95
	v_med3_f32 v235, v235, s62, v95
	v_med3_f32 v236, v236, s62, v95
	v_med3_f32 v237, v237, s62, v95
	v_med3_f32 v238, v238, s62, v95
	v_med3_f32 v239, v239, s62, v95
	v_med3_f32 v240, v240, s62, v95
	v_med3_f32 v241, v241, s62, v95
	v_mov_b32_e32 v242, 0
	v_mov_b32_e32 v243, 0
	v_mov_b32_e32 v244, 0
	v_mov_b32_e32 v245, 0
	v_cvt_pk_fp8_f32 v242, v226, v227
	v_cvt_pk_fp8_f32 v243, v230, v231
	v_cvt_pk_fp8_f32 v244, v234, v235
	v_cvt_pk_fp8_f32 v245, v238, v239
	v_cvt_pk_fp8_f32 v242, v228, v229 op_sel:[0,0,1]
	v_cvt_pk_fp8_f32 v243, v232, v233 op_sel:[0,0,1]
	v_cvt_pk_fp8_f32 v244, v236, v237 op_sel:[0,0,1]
	v_cvt_pk_fp8_f32 v245, v240, v241 op_sel:[0,0,1]
	s_nop 0
	global_store_dwordx4 v92, v[242:245], s[6:7]
	s_waitcnt vmcnt(12)
	v_mul_f32_e32 v144, v50, v144
	v_mul_f32_e32 v145, v50, v145
	v_mul_f32_e32 v146, v50, v146
	v_mul_f32_e32 v147, v50, v147
	ds_write_b128 v209, v[144:147]
	v_mul_f32_e32 v148, v51, v148
	v_mul_f32_e32 v149, v51, v149
	v_mul_f32_e32 v150, v51, v150
	v_mul_f32_e32 v151, v51, v151
	ds_write_b128 v209, v[148:151] offset:1024
	v_mul_f32_e32 v152, v52, v152
	v_mul_f32_e32 v153, v52, v153
	v_mul_f32_e32 v154, v52, v154
	v_mul_f32_e32 v155, v52, v155
	ds_write_b128 v209, v[152:155] offset:2048
	v_mul_f32_e32 v156, v53, v156
	v_mul_f32_e32 v157, v53, v157
	v_mul_f32_e32 v158, v53, v158
	v_mul_f32_e32 v159, v53, v159
	ds_write_b128 v209, v[156:159] offset:3072
	v_mul_f32_e32 v160, v54, v160
	v_mul_f32_e32 v161, v54, v161
	v_mul_f32_e32 v162, v54, v162
	v_mul_f32_e32 v163, v54, v163
	ds_write_b128 v209, v[160:163] offset:4096
	v_mul_f32_e32 v164, v55, v164
	v_mul_f32_e32 v165, v55, v165
	v_mul_f32_e32 v166, v55, v166
	v_mul_f32_e32 v167, v55, v167
	ds_write_b128 v209, v[164:167] offset:5120
	v_mul_f32_e32 v168, v56, v168
	v_mul_f32_e32 v169, v56, v169
	v_mul_f32_e32 v170, v56, v170
	v_mul_f32_e32 v171, v56, v171
	ds_write_b128 v209, v[168:171] offset:6144
	v_mul_f32_e32 v172, v57, v172
	v_mul_f32_e32 v173, v57, v173
	v_mul_f32_e32 v174, v57, v174
	v_mul_f32_e32 v175, v57, v175
	ds_write_b128 v209, v[172:175] offset:7168
	s_waitcnt lgkmcnt(0)
	s_barrier
; template <int MAP, bool KS, bool KPERM = false>
; __device__ __forceinline__ void p0_transpose_item(const float* W, int K, int Nsrc, int nblk, bf16* WT, const float* ksA, const float* ksB, int ksplit, LAS float* scr, int item, int lane) {
;     const int kb = item / nblk, nb = item % nblk, k0 = 64 * kb, n0 = 32 * nb;
;     const int nr = n0 + (lane & 31); const int sc = MAP == 1 ? src_col_in(nr) : (MAP == 2 ? nat_dim(nr) : nr);
;     float v[32];
; #pragma unroll
;     for (int i = 0; i < 32; ++i) { const int k = k0 + 2 * i + (lane >> 5); const int ksrc = KPERM ? ((k & ~127) + nat_dim(k & 127)) : k;
;         v[i] = sc >= 0 ? W[(size_t)ksrc * Nsrc + sc] : 0.f; }
; #pragma unroll
;     for (int i = 0; i < 32; ++i) { const int kk = 2 * i + (lane >> 5); const int k = k0 + kk;
;         if (KS) v[i] *= (k < ksplit ? ksA[k] : ksB[k - ksplit]);
;         scr[kk * 33 + (lane & 31)] = v[i]; }
;     LDS_WAIT(); asm volatile("" ::: "memory");
;     const int c = lane & 7;
; #pragma unroll
;     for (int j = 0; j < 4; ++j) { const int n = (lane >> 3) + 8 * j; const LAS float* s = scr + (8 * c) * 33 + n;
;         v4u o; o.x = pk2(s[0 * 33], s[1 * 33]); o.y = pk2(s[2 * 33], s[3 * 33]); o.z = pk2(s[4 * 33], s[5 * 33]); o.w = pk2(s[6 * 33], s[7 * 33]);
;         *(GAS v4u*)(WT + (size_t)(n0 + n) * K + k0 + 8 * c) = o; }
;     LDS_WAIT(); asm volatile("" ::: "memory");
; }
;     const int pr = item >> 1, kb = 2 * (pr / nblk) + (item & 1), nb = pr % nblk, k0 = 64 * kb, n0 = 32 * nb;
;     const int nr = n0 + (lane & 31); const int sc = MAP == 1 ? src_col_in(nr) : nr;
;     float v[32];
; #pragma unroll
;     for (int i = 0; i < 32; ++i) v[i] = sc >= 0 ? W[(size_t)(k0 + 2 * i + (lane >> 5)) * Nsrc + sc] : 0.f;
; #pragma unroll
;     for (int i = 0; i < 32; ++i) { const int k = k0 + 2 * i + (lane >> 5); float x = v[i] * wscale; if (KS) x *= (k < ksplit ? ksA[k] : ksB[k - ksplit]); scr[(2 * i + (lane >> 5)) * 33 + (lane & 31)] = x; }
;     LDS_WAIT(); asm volatile("" ::: "memory");
;     const int c = lane & 7;
; #pragma unroll
;     for (int j = 0; j < 4; ++j) { const int n = (lane >> 3) + 8 * j; const LAS float* s = scr + (8 * c) * 33 + n;
;         const unsigned long long o = (unsigned long long)pg8::pk4_fp8(s[0 * 33], s[1 * 33], s[2 * 33], s[3 * 33]) | ((unsigned long long)pg8::pk4_fp8(s[4 * 33], s[5 * 33], s[6 * 33], s[7 * 33]) << 32);
	s_mov_b64 s[8:9], s[54:55]
	global_load_dwordx4 v[144:147], v75, s[8:9]
	s_add_u32 s8, s8, 0x8000
	s_addc_u32 s9, s9, 0
	global_load_dwordx4 v[148:151], v75, s[8:9]
	s_add_u32 s8, s8, 0x8000
	s_addc_u32 s9, s9, 0
	global_load_dwordx4 v[152:155], v75, s[8:9]
	s_add_u32 s8, s8, 0x8000
	s_addc_u32 s9, s9, 0
	global_load_dwordx4 v[156:159], v75, s[8:9]
	s_add_u32 s8, s8, 0x8000
	s_addc_u32 s9, s9, 0
	global_load_dwordx4 v[160:163], v75, s[8:9]
	s_add_u32 s8, s8, 0x8000
	s_addc_u32 s9, s9, 0
	global_load_dwordx4 v[164:167], v75, s[8:9]
	s_add_u32 s8, s8, 0x8000
	s_addc_u32 s9, s9, 0
	global_load_dwordx4 v[168:171], v75, s[8:9]
	s_add_u32 s8, s8, 0x8000
	s_addc_u32 s9, s9, 0
	global_load_dwordx4 v[172:175], v75, s[8:9]
	s_add_i32 s24, s23, 72
	s_mul_i32 s20, s24, 0x80000
	s_add_u32 s6, s52, s20
	s_addc_u32 s7, s53, 0
	s_cmp_lt_u32 s24, 16
	s_cselect_b32 s20, 1, 0
	s_sub_i32 s21, s24, 16
	s_bitcmp0_b32 s21, 2
	s_cselect_b32 s21, 1, 0
	s_cmp_lt_u32 s24, 40
	s_cselect_b32 s21, s21, 0
	s_or_b32 s20, s20, s21
	s_cmp_lg_u32 s20, 0
	s_cselect_b64 s[20:21], -1, 0
	v_cndmask_b32_e64 v91, v77, v81, s[20:21]
	v_cndmask_b32_e64 v92, v78, v82, s[20:21]
	ds_read_b32 v226, v211
	ds_read_b32 v227, v211 offset:512
	ds_read_b32 v228, v211 offset:1024
	ds_read_b32 v229, v211 offset:1536
	ds_read_b32 v230, v211 offset:2048
	ds_read_b32 v231, v211 offset:2560
	ds_read_b32 v232, v211 offset:3072
	ds_read_b32 v233, v211 offset:3584
	ds_read_b32 v234, v211 offset:4096
	ds_read_b32 v235, v211 offset:4608
	ds_read_b32 v236, v211 offset:5120
	ds_read_b32 v237, v211 offset:5632
	ds_read_b32 v238, v211 offset:6144
	ds_read_b32 v239, v211 offset:6656
	ds_read_b32 v240, v211 offset:7168
	ds_read_b32 v241, v211 offset:7680
	s_waitcnt lgkmcnt(0)
	v_max_f32_e32 v226, v226, v226
	v_max_f32_e32 v227, v227, v227
	v_max_f32_e32 v228, v228, v228
	v_max_f32_e32 v229, v229, v229
	v_max_f32_e32 v230, v230, v230
	v_max_f32_e32 v231, v231, v231
	v_max_f32_e32 v232, v232, v232
	v_max_f32_e32 v233, v233, v233
	v_max_f32_e32 v234, v234, v234
	v_max_f32_e32 v235, v235, v235
	v_max_f32_e32 v236, v236, v236
	v_max_f32_e32 v237, v237, v237
	v_max_f32_e32 v238, v238, v238
	v_max_f32_e32 v239, v239, v239
	v_max_f32_e32 v240, v240, v240
	v_max_f32_e32 v241, v241, v241
	v_med3_f32 v226, v226, s62, v95
	v_med3_f32 v227, v227, s62, v95
	v_med3_f32 v228, v228, s62, v95
	v_med3_f32 v229, v229, s62, v95
	v_med3_f32 v230, v230, s62, v95
	v_med3_f32 v231, v231, s62, v95
	v_med3_f32 v232, v232, s62, v95
	v_med3_f32 v233, v233, s62, v95
	v_med3_f32 v234, v234, s62, v95
	v_med3_f32 v235, v235, s62, v95
	v_med3_f32 v236, v236, s62, v95
	v_med3_f32 v237, v237, s62, v95
	v_med3_f32 v238, v238, s62, v95
	v_med3_f32 v239, v239, s62, v95
	v_med3_f32 v240, v240, s62, v95
	v_med3_f32 v241, v241, s62, v95
	v_mov_b32_e32 v242, 0
	v_mov_b32_e32 v243, 0
	v_mov_b32_e32 v244, 0
	v_mov_b32_e32 v245, 0
	v_cvt_pk_fp8_f32 v242, v226, v227
	v_cvt_pk_fp8_f32 v243, v230, v231
	v_cvt_pk_fp8_f32 v244, v234, v235
	v_cvt_pk_fp8_f32 v245, v238, v239
	v_cvt_pk_fp8_f32 v242, v228, v229 op_sel:[0,0,1]
	v_cvt_pk_fp8_f32 v243, v232, v233 op_sel:[0,0,1]
	v_cvt_pk_fp8_f32 v244, v236, v237 op_sel:[0,0,1]
	v_cvt_pk_fp8_f32 v245, v240, v241 op_sel:[0,0,1]
	s_nop 0
	global_store_dwordx4 v91, v[242:245], s[6:7]
	ds_read_b32 v226, v213
	ds_read_b32 v227, v213 offset:512
	ds_read_b32 v228, v213 offset:1024
	ds_read_b32 v229, v213 offset:1536
	ds_read_b32 v230, v213 offset:2048
	ds_read_b32 v231, v213 offset:2560
	ds_read_b32 v232, v213 offset:3072
	ds_read_b32 v233, v213 offset:3584
	ds_read_b32 v234, v213 offset:4096
	ds_read_b32 v235, v213 offset:4608
	ds_read_b32 v236, v213 offset:5120
	ds_read_b32 v237, v213 offset:5632
	ds_read_b32 v238, v213 offset:6144
	ds_read_b32 v239, v213 offset:6656
	ds_read_b32 v240, v213 offset:7168
	ds_read_b32 v241, v213 offset:7680
	s_waitcnt lgkmcnt(0)
	v_max_f32_e32 v226, v226, v226
	v_max_f32_e32 v227, v227, v227
	v_max_f32_e32 v228, v228, v228
	v_max_f32_e32 v229, v229, v229
	v_max_f32_e32 v230, v230, v230
	v_max_f32_e32 v231, v231, v231
	v_max_f32_e32 v232, v232, v232
	v_max_f32_e32 v233, v233, v233
	v_max_f32_e32 v234, v234, v234
	v_max_f32_e32 v235, v235, v235
	v_max_f32_e32 v236, v236, v236
	v_max_f32_e32 v237, v237, v237
	v_max_f32_e32 v238, v238, v238
	v_max_f32_e32 v239, v239, v239
	v_max_f32_e32 v240, v240, v240
	v_max_f32_e32 v241, v241, v241
	v_med3_f32 v226, v226, s62, v95
	v_med3_f32 v227, v227, s62, v95
	v_med3_f32 v228, v228, s62, v95
	v_med3_f32 v229, v229, s62, v95
	v_med3_f32 v230, v230, s62, v95
	v_med3_f32 v231, v231, s62, v95
	v_med3_f32 v232, v232, s62, v95
	v_med3_f32 v233, v233, s62, v95
	v_med3_f32 v234, v234, s62, v95
	v_med3_f32 v235, v235, s62, v95
	v_med3_f32 v236, v236, s62, v95
	v_med3_f32 v237, v237, s62, v95
	v_med3_f32 v238, v238, s62, v95
	v_med3_f32 v239, v239, s62, v95
	v_med3_f32 v240, v240, s62, v95
	v_med3_f32 v241, v241, s62, v95
	v_mov_b32_e32 v242, 0
	v_mov_b32_e32 v243, 0
	v_mov_b32_e32 v244, 0
	v_mov_b32_e32 v245, 0
	v_cvt_pk_fp8_f32 v242, v226, v227
	v_cvt_pk_fp8_f32 v243, v230, v231
	v_cvt_pk_fp8_f32 v244, v234, v235
	v_cvt_pk_fp8_f32 v245, v238, v239
	v_cvt_pk_fp8_f32 v242, v228, v229 op_sel:[0,0,1]
	v_cvt_pk_fp8_f32 v243, v232, v233 op_sel:[0,0,1]
	v_cvt_pk_fp8_f32 v244, v236, v237 op_sel:[0,0,1]
	v_cvt_pk_fp8_f32 v245, v240, v241 op_sel:[0,0,1]
	s_nop 0
	global_store_dwordx4 v92, v[242:245], s[6:7]
	s_waitcnt vmcnt(12)
	v_mul_f32_e32 v176, v50, v176
	v_mul_f32_e32 v177, v50, v177
	v_mul_f32_e32 v178, v50, v178
	v_mul_f32_e32 v179, v50, v179
	ds_write_b128 v210, v[176:179]
	v_mul_f32_e32 v180, v51, v180
	v_mul_f32_e32 v181, v51, v181
	v_mul_f32_e32 v182, v51, v182
	v_mul_f32_e32 v183, v51, v183
	ds_write_b128 v210, v[180:183] offset:1024
	v_mul_f32_e32 v184, v52, v184
	v_mul_f32_e32 v185, v52, v185
	v_mul_f32_e32 v186, v52, v186
	v_mul_f32_e32 v187, v52, v187
	ds_write_b128 v210, v[184:187] offset:2048
	v_mul_f32_e32 v188, v53, v188
	v_mul_f32_e32 v189, v53, v189
	v_mul_f32_e32 v190, v53, v190
	v_mul_f32_e32 v191, v53, v191
	ds_write_b128 v210, v[188:191] offset:3072
	v_mul_f32_e32 v192, v54, v192
	v_mul_f32_e32 v193, v54, v193
	v_mul_f32_e32 v194, v54, v194
	v_mul_f32_e32 v195, v54, v195
	ds_write_b128 v210, v[192:195] offset:4096
	v_mul_f32_e32 v196, v55, v196
	v_mul_f32_e32 v197, v55, v197
	v_mul_f32_e32 v198, v55, v198
	v_mul_f32_e32 v199, v55, v199
	ds_write_b128 v210, v[196:199] offset:5120
	v_mul_f32_e32 v200, v56, v200
	v_mul_f32_e32 v201, v56, v201
	v_mul_f32_e32 v202, v56, v202
	v_mul_f32_e32 v203, v56, v203
	ds_write_b128 v210, v[200:203] offset:6144
	v_mul_f32_e32 v204, v57, v204
	v_mul_f32_e32 v205, v57, v205
	v_mul_f32_e32 v206, v57, v206
	v_mul_f32_e32 v207, v57, v207
	ds_write_b128 v210, v[204:207] offset:7168
	s_waitcnt lgkmcnt(0)
	s_barrier
; template <int MAP, bool KS, bool KPERM = false>
; __device__ __forceinline__ void p0_transpose_item(const float* W, int K, int Nsrc, int nblk, bf16* WT, const float* ksA, const float* ksB, int ksplit, LAS float* scr, int item, int lane) {
;     const int kb = item / nblk, nb = item % nblk, k0 = 64 * kb, n0 = 32 * nb;
;     const int nr = n0 + (lane & 31); const int sc = MAP == 1 ? src_col_in(nr) : (MAP == 2 ? nat_dim(nr) : nr);
;     float v[32];
; #pragma unroll
;     for (int i = 0; i < 32; ++i) { const int k = k0 + 2 * i + (lane >> 5); const int ksrc = KPERM ? ((k & ~127) + nat_dim(k & 127)) : k;
;         v[i] = sc >= 0 ? W[(size_t)ksrc * Nsrc + sc] : 0.f; }
; #pragma unroll
;     for (int i = 0; i < 32; ++i) { const int kk = 2 * i + (lane >> 5); const int k = k0 + kk;
;         if (KS) v[i] *= (k < ksplit ? ksA[k] : ksB[k - ksplit]);
;         scr[kk * 33 + (lane & 31)] = v[i]; }
;     LDS_WAIT(); asm volatile("" ::: "memory");
;     const int c = lane & 7;
; #pragma unroll
;     for (int j = 0; j < 4; ++j) { const int n = (lane >> 3) + 8 * j; const LAS float* s = scr + (8 * c) * 33 + n;
;         v4u o; o.x = pk2(s[0 * 33], s[1 * 33]); o.y = pk2(s[2 * 33], s[3 * 33]); o.z = pk2(s[4 * 33], s[5 * 33]); o.w = pk2(s[6 * 33], s[7 * 33]);
;         *(GAS v4u*)(WT + (size_t)(n0 + n) * K + k0 + 8 * c) = o; }
;     LDS_WAIT(); asm volatile("" ::: "memory");
; }
;     const int pr = item >> 1, kb = 2 * (pr / nblk) + (item & 1), nb = pr % nblk, k0 = 64 * kb, n0 = 32 * nb;
;     const int nr = n0 + (lane & 31); const int sc = MAP == 1 ? src_col_in(nr) : nr;
;     float v[32];
; #pragma unroll
;     for (int i = 0; i < 32; ++i) v[i] = sc >= 0 ? W[(size_t)(k0 + 2 * i + (lane >> 5)) * Nsrc + sc] : 0.f;
; #pragma unroll
;     for (int i = 0; i < 32; ++i) { const int k = k0 + 2 * i + (lane >> 5); float x = v[i] * wscale; if (KS) x *= (k < ksplit ? ksA[k] : ksB[k - ksplit]); scr[(2 * i + (lane >> 5)) * 33 + (lane & 31)] = x; }
;     LDS_WAIT(); asm volatile("" ::: "memory");
;     const int c = lane & 7;
; #pragma unroll
;     for (int j = 0; j < 4; ++j) { const int n = (lane >> 3) + 8 * j; const LAS float* s = scr + (8 * c) * 33 + n;
;         const unsigned long long o = (unsigned long long)pg8::pk4_fp8(s[0 * 33], s[1 * 33], s[2 * 33], s[3 * 33]) | ((unsigned long long)pg8::pk4_fp8(s[4 * 33], s[5 * 33], s[6 * 33], s[7 * 33]) << 32);
	s_add_u32 s8, s54, 0x1000
	s_addc_u32 s9, s55, 0
	global_load_dwordx4 v[176:179], v75, s[8:9]
	s_add_u32 s8, s8, 0x8000
	s_addc_u32 s9, s9, 0
	global_load_dwordx4 v[180:183], v75, s[8:9]
	s_add_u32 s8, s8, 0x8000
	s_addc_u32 s9, s9, 0
	global_load_dwordx4 v[184:187], v75, s[8:9]
	s_add_u32 s8, s8, 0x8000
	s_addc_u32 s9, s9, 0
	global_load_dwordx4 v[188:191], v75, s[8:9]
	s_add_u32 s8, s8, 0x8000
	s_addc_u32 s9, s9, 0
	global_load_dwordx4 v[192:195], v75, s[8:9]
	s_add_u32 s8, s8, 0x8000
	s_addc_u32 s9, s9, 0
	global_load_dwordx4 v[196:199], v75, s[8:9]
	s_add_u32 s8, s8, 0x8000
	s_addc_u32 s9, s9, 0
	global_load_dwordx4 v[200:203], v75, s[8:9]
	s_add_u32 s8, s8, 0x8000
	s_addc_u32 s9, s9, 0
	global_load_dwordx4 v[204:207], v75, s[8:9]
	s_add_i32 s24, s23, 80
	s_mul_i32 s20, s24, 0x80000
	s_add_u32 s6, s52, s20
	s_addc_u32 s7, s53, 0
	s_cmp_lt_u32 s24, 16
	s_cselect_b32 s20, 1, 0
	s_sub_i32 s21, s24, 16
	s_bitcmp0_b32 s21, 2
	s_cselect_b32 s21, 1, 0
	s_cmp_lt_u32 s24, 40
	s_cselect_b32 s21, s21, 0
	s_or_b32 s20, s20, s21
	s_cmp_lg_u32 s20, 0
	s_cselect_b64 s[20:21], -1, 0
	v_cndmask_b32_e64 v91, v77, v81, s[20:21]
	v_cndmask_b32_e64 v92, v78, v82, s[20:21]
	ds_read_b32 v226, v212
	ds_read_b32 v227, v212 offset:512
	ds_read_b32 v228, v212 offset:1024
	ds_read_b32 v229, v212 offset:1536
	ds_read_b32 v230, v212 offset:2048
	ds_read_b32 v231, v212 offset:2560
	ds_read_b32 v232, v212 offset:3072
	ds_read_b32 v233, v212 offset:3584
	ds_read_b32 v234, v212 offset:4096
	ds_read_b32 v235, v212 offset:4608
	ds_read_b32 v236, v212 offset:5120
	ds_read_b32 v237, v212 offset:5632
	ds_read_b32 v238, v212 offset:6144
	ds_read_b32 v239, v212 offset:6656
	ds_read_b32 v240, v212 offset:7168
	ds_read_b32 v241, v212 offset:7680
	s_waitcnt lgkmcnt(0)
	v_max_f32_e32 v226, v226, v226
	v_max_f32_e32 v227, v227, v227
	v_max_f32_e32 v228, v228, v228
	v_max_f32_e32 v229, v229, v229
	v_max_f32_e32 v230, v230, v230
	v_max_f32_e32 v231, v231, v231
	v_max_f32_e32 v232, v232, v232
	v_max_f32_e32 v233, v233, v233
	v_max_f32_e32 v234, v234, v234
	v_max_f32_e32 v235, v235, v235
	v_max_f32_e32 v236, v236, v236
	v_max_f32_e32 v237, v237, v237
	v_max_f32_e32 v238, v238, v238
	v_max_f32_e32 v239, v239, v239
	v_max_f32_e32 v240, v240, v240
	v_max_f32_e32 v241, v241, v241
	v_med3_f32 v226, v226, s62, v95
	v_med3_f32 v227, v227, s62, v95
	v_med3_f32 v228, v228, s62, v95
	v_med3_f32 v229, v229, s62, v95
	v_med3_f32 v230, v230, s62, v95
	v_med3_f32 v231, v231, s62, v95
	v_med3_f32 v232, v232, s62, v95
	v_med3_f32 v233, v233, s62, v95
	v_med3_f32 v234, v234, s62, v95
	v_med3_f32 v235, v235, s62, v95
	v_med3_f32 v236, v236, s62, v95
	v_med3_f32 v237, v237, s62, v95
	v_med3_f32 v238, v238, s62, v95
	v_med3_f32 v239, v239, s62, v95
	v_med3_f32 v240, v240, s62, v95
	v_med3_f32 v241, v241, s62, v95
	v_mov_b32_e32 v242, 0
	v_mov_b32_e32 v243, 0
	v_mov_b32_e32 v244, 0
	v_mov_b32_e32 v245, 0
	v_cvt_pk_fp8_f32 v242, v226, v227
	v_cvt_pk_fp8_f32 v243, v230, v231
	v_cvt_pk_fp8_f32 v244, v234, v235
	v_cvt_pk_fp8_f32 v245, v238, v239
	v_cvt_pk_fp8_f32 v242, v228, v229 op_sel:[0,0,1]
	v_cvt_pk_fp8_f32 v243, v232, v233 op_sel:[0,0,1]
	v_cvt_pk_fp8_f32 v244, v236, v237 op_sel:[0,0,1]
	v_cvt_pk_fp8_f32 v245, v240, v241 op_sel:[0,0,1]
	s_nop 0
	global_store_dwordx4 v91, v[242:245], s[6:7]
	ds_read_b32 v226, v214
	ds_read_b32 v227, v214 offset:512
	ds_read_b32 v228, v214 offset:1024
	ds_read_b32 v229, v214 offset:1536
	ds_read_b32 v230, v214 offset:2048
	ds_read_b32 v231, v214 offset:2560
	ds_read_b32 v232, v214 offset:3072
	ds_read_b32 v233, v214 offset:3584
	ds_read_b32 v234, v214 offset:4096
	ds_read_b32 v235, v214 offset:4608
	ds_read_b32 v236, v214 offset:5120
	ds_read_b32 v237, v214 offset:5632
	ds_read_b32 v238, v214 offset:6144
	ds_read_b32 v239, v214 offset:6656
	ds_read_b32 v240, v214 offset:7168
	ds_read_b32 v241, v214 offset:7680
	s_waitcnt lgkmcnt(0)
	v_max_f32_e32 v226, v226, v226
	v_max_f32_e32 v227, v227, v227
	v_max_f32_e32 v228, v228, v228
	v_max_f32_e32 v229, v229, v229
	v_max_f32_e32 v230, v230, v230
	v_max_f32_e32 v231, v231, v231
	v_max_f32_e32 v232, v232, v232
	v_max_f32_e32 v233, v233, v233
	v_max_f32_e32 v234, v234, v234
	v_max_f32_e32 v235, v235, v235
	v_max_f32_e32 v236, v236, v236
	v_max_f32_e32 v237, v237, v237
	v_max_f32_e32 v238, v238, v238
	v_max_f32_e32 v239, v239, v239
	v_max_f32_e32 v240, v240, v240
	v_max_f32_e32 v241, v241, v241
	v_med3_f32 v226, v226, s62, v95
	v_med3_f32 v227, v227, s62, v95
	v_med3_f32 v228, v228, s62, v95
	v_med3_f32 v229, v229, s62, v95
	v_med3_f32 v230, v230, s62, v95
	v_med3_f32 v231, v231, s62, v95
	v_med3_f32 v232, v232, s62, v95
	v_med3_f32 v233, v233, s62, v95
	v_med3_f32 v234, v234, s62, v95
	v_med3_f32 v235, v235, s62, v95
	v_med3_f32 v236, v236, s62, v95
	v_med3_f32 v237, v237, s62, v95
	v_med3_f32 v238, v238, s62, v95
	v_med3_f32 v239, v239, s62, v95
	v_med3_f32 v240, v240, s62, v95
	v_med3_f32 v241, v241, s62, v95
	v_mov_b32_e32 v242, 0
	v_mov_b32_e32 v243, 0
	v_mov_b32_e32 v244, 0
	v_mov_b32_e32 v245, 0
	v_cvt_pk_fp8_f32 v242, v226, v227
	v_cvt_pk_fp8_f32 v243, v230, v231
	v_cvt_pk_fp8_f32 v244, v234, v235
	v_cvt_pk_fp8_f32 v245, v238, v239
	v_cvt_pk_fp8_f32 v242, v228, v229 op_sel:[0,0,1]
	v_cvt_pk_fp8_f32 v243, v232, v233 op_sel:[0,0,1]
	v_cvt_pk_fp8_f32 v244, v236, v237 op_sel:[0,0,1]
	v_cvt_pk_fp8_f32 v245, v240, v241 op_sel:[0,0,1]
	s_nop 0
	global_store_dwordx4 v92, v[242:245], s[6:7]
	s_waitcnt vmcnt(12)
	v_mul_f32_e32 v144, v58, v144
	v_mul_f32_e32 v145, v58, v145
	v_mul_f32_e32 v146, v58, v146
	v_mul_f32_e32 v147, v58, v147
	ds_write_b128 v209, v[144:147]
	v_mul_f32_e32 v148, v59, v148
	v_mul_f32_e32 v149, v59, v149
	v_mul_f32_e32 v150, v59, v150
	v_mul_f32_e32 v151, v59, v151
	ds_write_b128 v209, v[148:151] offset:1024
	v_mul_f32_e32 v152, v60, v152
	v_mul_f32_e32 v153, v60, v153
	v_mul_f32_e32 v154, v60, v154
	v_mul_f32_e32 v155, v60, v155
	ds_write_b128 v209, v[152:155] offset:2048
	v_mul_f32_e32 v156, v61, v156
	v_mul_f32_e32 v157, v61, v157
	v_mul_f32_e32 v158, v61, v158
	v_mul_f32_e32 v159, v61, v159
	ds_write_b128 v209, v[156:159] offset:3072
	v_mul_f32_e32 v160, v62, v160
	v_mul_f32_e32 v161, v62, v161
	v_mul_f32_e32 v162, v62, v162
	v_mul_f32_e32 v163, v62, v163
	ds_write_b128 v209, v[160:163] offset:4096
	v_mul_f32_e32 v164, v63, v164
	v_mul_f32_e32 v165, v63, v165
	v_mul_f32_e32 v166, v63, v166
	v_mul_f32_e32 v167, v63, v167
	ds_write_b128 v209, v[164:167] offset:5120
	v_mul_f32_e32 v168, v64, v168
	v_mul_f32_e32 v169, v64, v169
	v_mul_f32_e32 v170, v64, v170
	v_mul_f32_e32 v171, v64, v171
	ds_write_b128 v209, v[168:171] offset:6144
	v_mul_f32_e32 v172, v65, v172
	v_mul_f32_e32 v173, v65, v173
	v_mul_f32_e32 v174, v65, v174
	v_mul_f32_e32 v175, v65, v175
	ds_write_b128 v209, v[172:175] offset:7168
	s_waitcnt lgkmcnt(0)
	s_barrier
; #define GAS __attribute__((address_space(1)))
; #define LAS __attribute__((address_space(3)))
; #define LDS_WAIT() asm volatile("s_waitcnt lgkmcnt(0)" ::: "memory")
; __device__ __forceinline__ unsigned pk2(float lo, float hi) { return f2bf(lo) | (f2bf(hi) << 16); }
; __device__ __forceinline__ int nat_dim(int p) { return (p >> 1) + 64 * (p & 1); }
; template <int MAP, bool KS, bool KPERM = false>
; __device__ __forceinline__ void p0_transpose_item(const float* W, int K, int Nsrc, int nblk, bf16* WT, const float* ksA, const float* ksB, int ksplit, LAS float* scr, int item, int lane) {
;     const int kb = item / nblk, nb = item % nblk, k0 = 64 * kb, n0 = 32 * nb;
;     const int nr = n0 + (lane & 31); const int sc = MAP == 1 ? src_col_in(nr) : (MAP == 2 ? nat_dim(nr) : nr);
;     float v[32];
; #pragma unroll
;     for (int i = 0; i < 32; ++i) { const int k = k0 + 2 * i + (lane >> 5); const int ksrc = KPERM ? ((k & ~127) + nat_dim(k & 127)) : k;
;         v[i] = sc >= 0 ? W[(size_t)ksrc * Nsrc + sc] : 0.f; }
; #pragma unroll
;     for (int i = 0; i < 32; ++i) { const int kk = 2 * i + (lane >> 5); const int k = k0 + kk;
;         if (KS) v[i] *= (k < ksplit ? ksA[k] : ksB[k - ksplit]);
;         scr[kk * 33 + (lane & 31)] = v[i]; }
;     LDS_WAIT(); asm volatile("" ::: "memory");
;     const int c = lane & 7;
; #pragma unroll
;     for (int j = 0; j < 4; ++j) { const int n = (lane >> 3) + 8 * j; const LAS float* s = scr + (8 * c) * 33 + n;
;         v4u o; o.x = pk2(s[0 * 33], s[1 * 33]); o.y = pk2(s[2 * 33], s[3 * 33]); o.z = pk2(s[4 * 33], s[5 * 33]); o.w = pk2(s[6 * 33], s[7 * 33]);
;         *(GAS v4u*)(WT + (size_t)(n0 + n) * K + k0 + 8 * c) = o; }
;     LDS_WAIT(); asm volatile("" ::: "memory");
; }
; __global__ void __launch_bounds__(NWAVES * 64, 2) hybrid_fwd(Args args) {
;     ...
;             if (r < I_O) { if (l >= WO_F8_FROM) p0_transpose_item_f8<true>(args.in[13] + (size_t)l * DM * DM, DM, DM, DM / 32, (unsigned char*)(ws + WS_WO + l * SZ_WO), 64.f, args.in[6] + l * 2048, args.in[12] + l * 2048, 2048, scr, r, lane);
;                 else p0_transpose_item<0, true>(args.in[13] + (size_t)l * DM * DM, DM, DM, DM / 32, (bf16*)(ws + WS_WO + l * SZ_WO), args.in[6] + l * 2048, args.in[12] + l * 2048, 2048, scr, r, lane); continue; } r -= I_O;
	s_add_u32 s8, s54, 0x2000
	s_addc_u32 s9, s55, 0
	global_load_dwordx4 v[144:147], v75, s[8:9]
	s_add_u32 s8, s8, 0x8000
	s_addc_u32 s9, s9, 0
	global_load_dwordx4 v[148:151], v75, s[8:9]
	s_add_u32 s8, s8, 0x8000
	s_addc_u32 s9, s9, 0
	global_load_dwordx4 v[152:155], v75, s[8:9]
	s_add_u32 s8, s8, 0x8000
	s_addc_u32 s9, s9, 0
	global_load_dwordx4 v[156:159], v75, s[8:9]
	s_add_u32 s8, s8, 0x8000
	s_addc_u32 s9, s9, 0
	global_load_dwordx4 v[160:163], v75, s[8:9]
	s_add_u32 s8, s8, 0x8000
	s_addc_u32 s9, s9, 0
	global_load_dwordx4 v[164:167], v75, s[8:9]
	s_add_u32 s8, s8, 0x8000
	s_addc_u32 s9, s9, 0
	global_load_dwordx4 v[168:171], v75, s[8:9]
	s_add_u32 s8, s8, 0x8000
	s_addc_u32 s9, s9, 0
	global_load_dwordx4 v[172:175], v75, s[8:9]
	s_mov_b64 s[6:7], s[56:57]
	ds_read_b32 v226, v112
	ds_read_b32 v227, v112 offset:512
	ds_read_b32 v228, v112 offset:1024
	ds_read_b32 v229, v112 offset:1536
	ds_read_b32 v230, v112 offset:2048
	ds_read_b32 v231, v112 offset:2560
	ds_read_b32 v232, v112 offset:3072
	ds_read_b32 v233, v112 offset:3584
	s_waitcnt lgkmcnt(0)
	v_bfe_u32 v120, v226, 16, 1
	v_bfe_u32 v121, v227, 16, 1
	v_bfe_u32 v122, v228, 16, 1
	v_bfe_u32 v123, v229, 16, 1
	v_bfe_u32 v124, v230, 16, 1
	v_bfe_u32 v125, v231, 16, 1
	v_bfe_u32 v126, v232, 16, 1
	v_bfe_u32 v127, v233, 16, 1
	v_add3_u32 v226, v226, v120, s63
	v_add3_u32 v227, v227, v121, s63
	v_add3_u32 v228, v228, v122, s63
	v_add3_u32 v229, v229, v123, s63
	v_add3_u32 v230, v230, v124, s63
	v_add3_u32 v231, v231, v125, s63
	v_add3_u32 v232, v232, v126, s63
	v_add3_u32 v233, v233, v127, s63
	v_perm_b32 v242, v227, v226, s64
	v_perm_b32 v243, v229, v228, s64
	v_perm_b32 v244, v231, v230, s64
	v_perm_b32 v245, v233, v232, s64
	s_nop 0
	global_store_dwordx4 v83, v[242:245], s[6:7]
	ds_read_b32 v226, v114
	ds_read_b32 v227, v114 offset:512
	ds_read_b32 v228, v114 offset:1024
	ds_read_b32 v229, v114 offset:1536
	ds_read_b32 v230, v114 offset:2048
	ds_read_b32 v231, v114 offset:2560
	ds_read_b32 v232, v114 offset:3072
	ds_read_b32 v233, v114 offset:3584
	s_waitcnt lgkmcnt(0)
	v_bfe_u32 v120, v226, 16, 1
	v_bfe_u32 v121, v227, 16, 1
	v_bfe_u32 v122, v228, 16, 1
	v_bfe_u32 v123, v229, 16, 1
	v_bfe_u32 v124, v230, 16, 1
	v_bfe_u32 v125, v231, 16, 1
	v_bfe_u32 v126, v232, 16, 1
	v_bfe_u32 v127, v233, 16, 1
	v_add3_u32 v226, v226, v120, s63
	v_add3_u32 v227, v227, v121, s63
	v_add3_u32 v228, v228, v122, s63
	v_add3_u32 v229, v229, v123, s63
	v_add3_u32 v230, v230, v124, s63
	v_add3_u32 v231, v231, v125, s63
	v_add3_u32 v232, v232, v126, s63
	v_add3_u32 v233, v233, v127, s63
	v_perm_b32 v242, v227, v226, s64
	v_perm_b32 v243, v229, v228, s64
	v_perm_b32 v244, v231, v230, s64
	v_perm_b32 v245, v233, v232, s64
	s_nop 0
	global_store_dwordx4 v84, v[242:245], s[6:7]
	ds_read_b32 v226, v116
	ds_read_b32 v227, v116 offset:512
	ds_read_b32 v228, v116 offset:1024
	ds_read_b32 v229, v116 offset:1536
	ds_read_b32 v230, v116 offset:2048
	ds_read_b32 v231, v116 offset:2560
	ds_read_b32 v232, v116 offset:3072
	ds_read_b32 v233, v116 offset:3584
	s_waitcnt lgkmcnt(0)
	v_bfe_u32 v120, v226, 16, 1
	v_bfe_u32 v121, v227, 16, 1
	v_bfe_u32 v122, v228, 16, 1
	v_bfe_u32 v123, v229, 16, 1
	v_bfe_u32 v124, v230, 16, 1
	v_bfe_u32 v125, v231, 16, 1
	v_bfe_u32 v126, v232, 16, 1
	v_bfe_u32 v127, v233, 16, 1
	v_add3_u32 v226, v226, v120, s63
	v_add3_u32 v227, v227, v121, s63
	v_add3_u32 v228, v228, v122, s63
	v_add3_u32 v229, v229, v123, s63
	v_add3_u32 v230, v230, v124, s63
	v_add3_u32 v231, v231, v125, s63
	v_add3_u32 v232, v232, v126, s63
	v_add3_u32 v233, v233, v127, s63
	v_perm_b32 v242, v227, v226, s64
	v_perm_b32 v243, v229, v228, s64
	v_perm_b32 v244, v231, v230, s64
	v_perm_b32 v245, v233, v232, s64
	s_nop 0
	global_store_dwordx4 v85, v[242:245], s[6:7]
	ds_read_b32 v226, v118
	ds_read_b32 v227, v118 offset:512
	ds_read_b32 v228, v118 offset:1024
	ds_read_b32 v229, v118 offset:1536
	ds_read_b32 v230, v118 offset:2048
	ds_read_b32 v231, v118 offset:2560
	ds_read_b32 v232, v118 offset:3072
	ds_read_b32 v233, v118 offset:3584
	s_waitcnt lgkmcnt(0)
	v_bfe_u32 v120, v226, 16, 1
	v_bfe_u32 v121, v227, 16, 1
	v_bfe_u32 v122, v228, 16, 1
	v_bfe_u32 v123, v229, 16, 1
	v_bfe_u32 v124, v230, 16, 1
	v_bfe_u32 v125, v231, 16, 1
	v_bfe_u32 v126, v232, 16, 1
	v_bfe_u32 v127, v233, 16, 1
	v_add3_u32 v226, v226, v120, s63
	v_add3_u32 v227, v227, v121, s63
	v_add3_u32 v228, v228, v122, s63
	v_add3_u32 v229, v229, v123, s63
	v_add3_u32 v230, v230, v124, s63
	v_add3_u32 v231, v231, v125, s63
	v_add3_u32 v232, v232, v126, s63
	v_add3_u32 v233, v233, v127, s63
	v_perm_b32 v242, v227, v226, s64
	v_perm_b32 v243, v229, v228, s64
	v_perm_b32 v244, v231, v230, s64
	v_perm_b32 v245, v233, v232, s64
	s_nop 0
	global_store_dwordx4 v86, v[242:245], s[6:7]
	s_waitcnt vmcnt(14)
	v_mul_f32_e32 v176, v58, v176
	v_mul_f32_e32 v177, v58, v177
	v_mul_f32_e32 v178, v58, v178
	v_mul_f32_e32 v179, v58, v179
	ds_write_b128 v210, v[176:179]
	v_mul_f32_e32 v180, v59, v180
	v_mul_f32_e32 v181, v59, v181
	v_mul_f32_e32 v182, v59, v182
	v_mul_f32_e32 v183, v59, v183
	ds_write_b128 v210, v[180:183] offset:1024
	v_mul_f32_e32 v184, v60, v184
	v_mul_f32_e32 v185, v60, v185
	v_mul_f32_e32 v186, v60, v186
	v_mul_f32_e32 v187, v60, v187
	ds_write_b128 v210, v[184:187] offset:2048
	v_mul_f32_e32 v188, v61, v188
	v_mul_f32_e32 v189, v61, v189
	v_mul_f32_e32 v190, v61, v190
	v_mul_f32_e32 v191, v61, v191
	ds_write_b128 v210, v[188:191] offset:3072
	v_mul_f32_e32 v192, v62, v192
	v_mul_f32_e32 v193, v62, v193
	v_mul_f32_e32 v194, v62, v194
	v_mul_f32_e32 v195, v62, v195
	ds_write_b128 v210, v[192:195] offset:4096
	v_mul_f32_e32 v196, v63, v196
	v_mul_f32_e32 v197, v63, v197
	v_mul_f32_e32 v198, v63, v198
	v_mul_f32_e32 v199, v63, v199
	ds_write_b128 v210, v[196:199] offset:5120
	v_mul_f32_e32 v200, v64, v200
	v_mul_f32_e32 v201, v64, v201
	v_mul_f32_e32 v202, v64, v202
	v_mul_f32_e32 v203, v64, v203
	ds_write_b128 v210, v[200:203] offset:6144
	v_mul_f32_e32 v204, v65, v204
	v_mul_f32_e32 v205, v65, v205
	v_mul_f32_e32 v206, v65, v206
	v_mul_f32_e32 v207, v65, v207
	ds_write_b128 v210, v[204:207] offset:7168
	s_waitcnt lgkmcnt(0)
	s_barrier
; #define GAS __attribute__((address_space(1)))
; #define LAS __attribute__((address_space(3)))
; #define LDS_WAIT() asm volatile("s_waitcnt lgkmcnt(0)" ::: "memory")
; __device__ __forceinline__ unsigned pk2(float lo, float hi) { return f2bf(lo) | (f2bf(hi) << 16); }
; __device__ __forceinline__ int nat_dim(int p) { return (p >> 1) + 64 * (p & 1); }
; template <int MAP, bool KS, bool KPERM = false>
; __device__ __forceinline__ void p0_transpose_item(const float* W, int K, int Nsrc, int nblk, bf16* WT, const float* ksA, const float* ksB, int ksplit, LAS float* scr, int item, int lane) {
;     const int kb = item / nblk, nb = item % nblk, k0 = 64 * kb, n0 = 32 * nb;
;     const int nr = n0 + (lane & 31); const int sc = MAP == 1 ? src_col_in(nr) : (MAP == 2 ? nat_dim(nr) : nr);
;     float v[32];
; #pragma unroll
;     for (int i = 0; i < 32; ++i) { const int k = k0 + 2 * i + (lane >> 5); const int ksrc = KPERM ? ((k & ~127) + nat_dim(k & 127)) : k;
;         v[i] = sc >= 0 ? W[(size_t)ksrc * Nsrc + sc] : 0.f; }
; #pragma unroll
;     for (int i = 0; i < 32; ++i) { const int kk = 2 * i + (lane >> 5); const int k = k0 + kk;
;         if (KS) v[i] *= (k < ksplit ? ksA[k] : ksB[k - ksplit]);
;         scr[kk * 33 + (lane & 31)] = v[i]; }
;     LDS_WAIT(); asm volatile("" ::: "memory");
;     const int c = lane & 7;
; #pragma unroll
;     for (int j = 0; j < 4; ++j) { const int n = (lane >> 3) + 8 * j; const LAS float* s = scr + (8 * c) * 33 + n;
;         v4u o; o.x = pk2(s[0 * 33], s[1 * 33]); o.y = pk2(s[2 * 33], s[3 * 33]); o.z = pk2(s[4 * 33], s[5 * 33]); o.w = pk2(s[6 * 33], s[7 * 33]);
;         *(GAS v4u*)(WT + (size_t)(n0 + n) * K + k0 + 8 * c) = o; }
;     LDS_WAIT(); asm volatile("" ::: "memory");
; }
; __global__ void __launch_bounds__(NWAVES * 64, 2) hybrid_fwd(Args args) {
;     ...
;             if (r < I_O) { if (l >= WO_F8_FROM) p0_transpose_item_f8<true>(args.in[13] + (size_t)l * DM * DM, DM, DM, DM / 32, (unsigned char*)(ws + WS_WO + l * SZ_WO), 64.f, args.in[6] + l * 2048, args.in[12] + l * 2048, 2048, scr, r, lane);
;                 else p0_transpose_item<0, true>(args.in[13] + (size_t)l * DM * DM, DM, DM, DM / 32, (bf16*)(ws + WS_WO + l * SZ_WO), args.in[6] + l * 2048, args.in[12] + l * 2048, 2048, scr, r, lane); continue; } r -= I_O;
	s_add_u32 s8, s54, 0x3000
	s_addc_u32 s9, s55, 0
	global_load_dwordx4 v[176:179], v75, s[8:9]
	s_add_u32 s8, s8, 0x8000
	s_addc_u32 s9, s9, 0
	global_load_dwordx4 v[180:183], v75, s[8:9]
	s_add_u32 s8, s8, 0x8000
	s_addc_u32 s9, s9, 0
	global_load_dwordx4 v[184:187], v75, s[8:9]
	s_add_u32 s8, s8, 0x8000
	s_addc_u32 s9, s9, 0
	global_load_dwordx4 v[188:191], v75, s[8:9]
	s_add_u32 s8, s8, 0x8000
	s_addc_u32 s9, s9, 0
	global_load_dwordx4 v[192:195], v75, s[8:9]
	s_add_u32 s8, s8, 0x8000
	s_addc_u32 s9, s9, 0
	global_load_dwordx4 v[196:199], v75, s[8:9]
	s_add_u32 s8, s8, 0x8000
	s_addc_u32 s9, s9, 0
	global_load_dwordx4 v[200:203], v75, s[8:9]
	s_add_u32 s8, s8, 0x8000
	s_addc_u32 s9, s9, 0
	global_load_dwordx4 v[204:207], v75, s[8:9]
	s_add_u32 s6, s56, 0x800000
	s_addc_u32 s7, s57, 0
	ds_read_b32 v226, v113
	ds_read_b32 v227, v113 offset:512
	ds_read_b32 v228, v113 offset:1024
	ds_read_b32 v229, v113 offset:1536
	ds_read_b32 v230, v113 offset:2048
	ds_read_b32 v231, v113 offset:2560
	ds_read_b32 v232, v113 offset:3072
	ds_read_b32 v233, v113 offset:3584
	s_waitcnt lgkmcnt(0)
	v_bfe_u32 v120, v226, 16, 1
	v_bfe_u32 v121, v227, 16, 1
	v_bfe_u32 v122, v228, 16, 1
	v_bfe_u32 v123, v229, 16, 1
	v_bfe_u32 v124, v230, 16, 1
	v_bfe_u32 v125, v231, 16, 1
	v_bfe_u32 v126, v232, 16, 1
	v_bfe_u32 v127, v233, 16, 1
	v_add3_u32 v226, v226, v120, s63
	v_add3_u32 v227, v227, v121, s63
	v_add3_u32 v228, v228, v122, s63
	v_add3_u32 v229, v229, v123, s63
	v_add3_u32 v230, v230, v124, s63
	v_add3_u32 v231, v231, v125, s63
	v_add3_u32 v232, v232, v126, s63
	v_add3_u32 v233, v233, v127, s63
	v_perm_b32 v242, v227, v226, s64
	v_perm_b32 v243, v229, v228, s64
	v_perm_b32 v244, v231, v230, s64
	v_perm_b32 v245, v233, v232, s64
	s_nop 0
	global_store_dwordx4 v83, v[242:245], s[6:7]
	ds_read_b32 v226, v115
	ds_read_b32 v227, v115 offset:512
	ds_read_b32 v228, v115 offset:1024
	ds_read_b32 v229, v115 offset:1536
	ds_read_b32 v230, v115 offset:2048
	ds_read_b32 v231, v115 offset:2560
	ds_read_b32 v232, v115 offset:3072
	ds_read_b32 v233, v115 offset:3584
	s_waitcnt lgkmcnt(0)
	v_bfe_u32 v120, v226, 16, 1
	v_bfe_u32 v121, v227, 16, 1
	v_bfe_u32 v122, v228, 16, 1
	v_bfe_u32 v123, v229, 16, 1
	v_bfe_u32 v124, v230, 16, 1
	v_bfe_u32 v125, v231, 16, 1
	v_bfe_u32 v126, v232, 16, 1
	v_bfe_u32 v127, v233, 16, 1
	v_add3_u32 v226, v226, v120, s63
	v_add3_u32 v227, v227, v121, s63
	v_add3_u32 v228, v228, v122, s63
	v_add3_u32 v229, v229, v123, s63
	v_add3_u32 v230, v230, v124, s63
	v_add3_u32 v231, v231, v125, s63
	v_add3_u32 v232, v232, v126, s63
	v_add3_u32 v233, v233, v127, s63
	v_perm_b32 v242, v227, v226, s64
	v_perm_b32 v243, v229, v228, s64
	v_perm_b32 v244, v231, v230, s64
	v_perm_b32 v245, v233, v232, s64
	s_nop 0
	global_store_dwordx4 v84, v[242:245], s[6:7]
	ds_read_b32 v226, v117
	ds_read_b32 v227, v117 offset:512
	ds_read_b32 v228, v117 offset:1024
	ds_read_b32 v229, v117 offset:1536
	ds_read_b32 v230, v117 offset:2048
	ds_read_b32 v231, v117 offset:2560
	ds_read_b32 v232, v117 offset:3072
	ds_read_b32 v233, v117 offset:3584
	s_waitcnt lgkmcnt(0)
	v_bfe_u32 v120, v226, 16, 1
	v_bfe_u32 v121, v227, 16, 1
	v_bfe_u32 v122, v228, 16, 1
	v_bfe_u32 v123, v229, 16, 1
	v_bfe_u32 v124, v230, 16, 1
	v_bfe_u32 v125, v231, 16, 1
	v_bfe_u32 v126, v232, 16, 1
	v_bfe_u32 v127, v233, 16, 1
	v_add3_u32 v226, v226, v120, s63
	v_add3_u32 v227, v227, v121, s63
	v_add3_u32 v228, v228, v122, s63
	v_add3_u32 v229, v229, v123, s63
	v_add3_u32 v230, v230, v124, s63
	v_add3_u32 v231, v231, v125, s63
	v_add3_u32 v232, v232, v126, s63
	v_add3_u32 v233, v233, v127, s63
	v_perm_b32 v242, v227, v226, s64
	v_perm_b32 v243, v229, v228, s64
	v_perm_b32 v244, v231, v230, s64
	v_perm_b32 v245, v233, v232, s64
	s_nop 0
	global_store_dwordx4 v85, v[242:245], s[6:7]
	ds_read_b32 v226, v119
	ds_read_b32 v227, v119 offset:512
	ds_read_b32 v228, v119 offset:1024
	ds_read_b32 v229, v119 offset:1536
	ds_read_b32 v230, v119 offset:2048
	ds_read_b32 v231, v119 offset:2560
	ds_read_b32 v232, v119 offset:3072
	ds_read_b32 v233, v119 offset:3584
	s_waitcnt lgkmcnt(0)
	v_bfe_u32 v120, v226, 16, 1
	v_bfe_u32 v121, v227, 16, 1
	v_bfe_u32 v122, v228, 16, 1
	v_bfe_u32 v123, v229, 16, 1
	v_bfe_u32 v124, v230, 16, 1
	v_bfe_u32 v125, v231, 16, 1
	v_bfe_u32 v126, v232, 16, 1
	v_bfe_u32 v127, v233, 16, 1
	v_add3_u32 v226, v226, v120, s63
	v_add3_u32 v227, v227, v121, s63
	v_add3_u32 v228, v228, v122, s63
	v_add3_u32 v229, v229, v123, s63
	v_add3_u32 v230, v230, v124, s63
	v_add3_u32 v231, v231, v125, s63
	v_add3_u32 v232, v232, v126, s63
	v_add3_u32 v233, v233, v127, s63
	v_perm_b32 v242, v227, v226, s64
	v_perm_b32 v243, v229, v228, s64
	v_perm_b32 v244, v231, v230, s64
	v_perm_b32 v245, v233, v232, s64
	s_nop 0
	global_store_dwordx4 v86, v[242:245], s[6:7]
	s_waitcnt vmcnt(16)
	v_mul_f32_e32 v144, v58, v144
	v_mul_f32_e32 v145, v58, v145
	v_mul_f32_e32 v146, v58, v146
	v_mul_f32_e32 v147, v58, v147
	ds_write_b128 v209, v[144:147]
	v_mul_f32_e32 v148, v59, v148
	v_mul_f32_e32 v149, v59, v149
	v_mul_f32_e32 v150, v59, v150
	v_mul_f32_e32 v151, v59, v151
	ds_write_b128 v209, v[148:151] offset:1024
	v_mul_f32_e32 v152, v60, v152
	v_mul_f32_e32 v153, v60, v153
	v_mul_f32_e32 v154, v60, v154
	v_mul_f32_e32 v155, v60, v155
	ds_write_b128 v209, v[152:155] offset:2048
	v_mul_f32_e32 v156, v61, v156
	v_mul_f32_e32 v157, v61, v157
	v_mul_f32_e32 v158, v61, v158
	v_mul_f32_e32 v159, v61, v159
	ds_write_b128 v209, v[156:159] offset:3072
	v_mul_f32_e32 v160, v62, v160
	v_mul_f32_e32 v161, v62, v161
	v_mul_f32_e32 v162, v62, v162
	v_mul_f32_e32 v163, v62, v163
	ds_write_b128 v209, v[160:163] offset:4096
	v_mul_f32_e32 v164, v63, v164
	v_mul_f32_e32 v165, v63, v165
	v_mul_f32_e32 v166, v63, v166
	v_mul_f32_e32 v167, v63, v167
	ds_write_b128 v209, v[164:167] offset:5120
	v_mul_f32_e32 v168, v64, v168
	v_mul_f32_e32 v169, v64, v169
	v_mul_f32_e32 v170, v64, v170
	v_mul_f32_e32 v171, v64, v171
	ds_write_b128 v209, v[168:171] offset:6144
	v_mul_f32_e32 v172, v65, v172
	v_mul_f32_e32 v173, v65, v173
	v_mul_f32_e32 v174, v65, v174
	v_mul_f32_e32 v175, v65, v175
	ds_write_b128 v209, v[172:175] offset:7168
	s_waitcnt lgkmcnt(0)
	s_barrier
; #define GAS __attribute__((address_space(1)))
; #define LAS __attribute__((address_space(3)))
; #define LDS_WAIT() asm volatile("s_waitcnt lgkmcnt(0)" ::: "memory")
; __device__ __forceinline__ unsigned pk2(float lo, float hi) { return f2bf(lo) | (f2bf(hi) << 16); }
; __device__ __forceinline__ int nat_dim(int p) { return (p >> 1) + 64 * (p & 1); }
; template <int MAP, bool KS, bool KPERM = false>
; __device__ __forceinline__ void p0_transpose_item(const float* W, int K, int Nsrc, int nblk, bf16* WT, const float* ksA, const float* ksB, int ksplit, LAS float* scr, int item, int lane) {
;     const int kb = item / nblk, nb = item % nblk, k0 = 64 * kb, n0 = 32 * nb;
;     const int nr = n0 + (lane & 31); const int sc = MAP == 1 ? src_col_in(nr) : (MAP == 2 ? nat_dim(nr) : nr);
;     float v[32];
; #pragma unroll
;     for (int i = 0; i < 32; ++i) { const int k = k0 + 2 * i + (lane >> 5); const int ksrc = KPERM ? ((k & ~127) + nat_dim(k & 127)) : k;
;         v[i] = sc >= 0 ? W[(size_t)ksrc * Nsrc + sc] : 0.f; }
; #pragma unroll
;     for (int i = 0; i < 32; ++i) { const int kk = 2 * i + (lane >> 5); const int k = k0 + kk;
;         if (KS) v[i] *= (k < ksplit ? ksA[k] : ksB[k - ksplit]);
;         scr[kk * 33 + (lane & 31)] = v[i]; }
;     LDS_WAIT(); asm volatile("" ::: "memory");
;     const int c = lane & 7;
; #pragma unroll
;     for (int j = 0; j < 4; ++j) { const int n = (lane >> 3) + 8 * j; const LAS float* s = scr + (8 * c) * 33 + n;
;         v4u o; o.x = pk2(s[0 * 33], s[1 * 33]); o.y = pk2(s[2 * 33], s[3 * 33]); o.z = pk2(s[4 * 33], s[5 * 33]); o.w = pk2(s[6 * 33], s[7 * 33]);
;         *(GAS v4u*)(WT + (size_t)(n0 + n) * K + k0 + 8 * c) = o; }
;     LDS_WAIT(); asm volatile("" ::: "memory");
; }
; __global__ void __launch_bounds__(NWAVES * 64, 2) hybrid_fwd(Args args) {
;     ...
;             if (r < I_O) { if (l >= WO_F8_FROM) p0_transpose_item_f8<true>(args.in[13] + (size_t)l * DM * DM, DM, DM, DM / 32, (unsigned char*)(ws + WS_WO + l * SZ_WO), 64.f, args.in[6] + l * 2048, args.in[12] + l * 2048, 2048, scr, r, lane);
;                 else p0_transpose_item<0, true>(args.in[13] + (size_t)l * DM * DM, DM, DM, DM / 32, (bf16*)(ws + WS_WO + l * SZ_WO), args.in[6] + l * 2048, args.in[12] + l * 2048, 2048, scr, r, lane); continue; } r -= I_O;
	s_add_u32 s6, s56, 0x1000000
	s_addc_u32 s7, s57, 0
	ds_read_b32 v226, v112
	ds_read_b32 v227, v112 offset:512
	ds_read_b32 v228, v112 offset:1024
	ds_read_b32 v229, v112 offset:1536
	ds_read_b32 v230, v112 offset:2048
	ds_read_b32 v231, v112 offset:2560
	ds_read_b32 v232, v112 offset:3072
	ds_read_b32 v233, v112 offset:3584
	s_waitcnt lgkmcnt(0)
	v_bfe_u32 v120, v226, 16, 1
	v_bfe_u32 v121, v227, 16, 1
	v_bfe_u32 v122, v228, 16, 1
	v_bfe_u32 v123, v229, 16, 1
	v_bfe_u32 v124, v230, 16, 1
	v_bfe_u32 v125, v231, 16, 1
	v_bfe_u32 v126, v232, 16, 1
	v_bfe_u32 v127, v233, 16, 1
	v_add3_u32 v226, v226, v120, s63
	v_add3_u32 v227, v227, v121, s63
	v_add3_u32 v228, v228, v122, s63
	v_add3_u32 v229, v229, v123, s63
	v_add3_u32 v230, v230, v124, s63
	v_add3_u32 v231, v231, v125, s63
	v_add3_u32 v232, v232, v126, s63
	v_add3_u32 v233, v233, v127, s63
	v_perm_b32 v242, v227, v226, s64
	v_perm_b32 v243, v229, v228, s64
	v_perm_b32 v244, v231, v230, s64
	v_perm_b32 v245, v233, v232, s64
	s_nop 0
	global_store_dwordx4 v83, v[242:245], s[6:7]
	ds_read_b32 v226, v114
	ds_read_b32 v227, v114 offset:512
	ds_read_b32 v228, v114 offset:1024
	ds_read_b32 v229, v114 offset:1536
	ds_read_b32 v230, v114 offset:2048
	ds_read_b32 v231, v114 offset:2560
	ds_read_b32 v232, v114 offset:3072
	ds_read_b32 v233, v114 offset:3584
	s_waitcnt lgkmcnt(0)
	v_bfe_u32 v120, v226, 16, 1
	v_bfe_u32 v121, v227, 16, 1
	v_bfe_u32 v122, v228, 16, 1
	v_bfe_u32 v123, v229, 16, 1
	v_bfe_u32 v124, v230, 16, 1
	v_bfe_u32 v125, v231, 16, 1
	v_bfe_u32 v126, v232, 16, 1
	v_bfe_u32 v127, v233, 16, 1
	v_add3_u32 v226, v226, v120, s63
	v_add3_u32 v227, v227, v121, s63
	v_add3_u32 v228, v228, v122, s63
	v_add3_u32 v229, v229, v123, s63
	v_add3_u32 v230, v230, v124, s63
	v_add3_u32 v231, v231, v125, s63
	v_add3_u32 v232, v232, v126, s63
	v_add3_u32 v233, v233, v127, s63
	v_perm_b32 v242, v227, v226, s64
	v_perm_b32 v243, v229, v228, s64
	v_perm_b32 v244, v231, v230, s64
	v_perm_b32 v245, v233, v232, s64
	s_nop 0
	global_store_dwordx4 v84, v[242:245], s[6:7]
	ds_read_b32 v226, v116
	ds_read_b32 v227, v116 offset:512
	ds_read_b32 v228, v116 offset:1024
	ds_read_b32 v229, v116 offset:1536
	ds_read_b32 v230, v116 offset:2048
	ds_read_b32 v231, v116 offset:2560
	ds_read_b32 v232, v116 offset:3072
	ds_read_b32 v233, v116 offset:3584
	s_waitcnt lgkmcnt(0)
	v_bfe_u32 v120, v226, 16, 1
	v_bfe_u32 v121, v227, 16, 1
	v_bfe_u32 v122, v228, 16, 1
	v_bfe_u32 v123, v229, 16, 1
	v_bfe_u32 v124, v230, 16, 1
	v_bfe_u32 v125, v231, 16, 1
	v_bfe_u32 v126, v232, 16, 1
	v_bfe_u32 v127, v233, 16, 1
	v_add3_u32 v226, v226, v120, s63
	v_add3_u32 v227, v227, v121, s63
	v_add3_u32 v228, v228, v122, s63
	v_add3_u32 v229, v229, v123, s63
	v_add3_u32 v230, v230, v124, s63
	v_add3_u32 v231, v231, v125, s63
	v_add3_u32 v232, v232, v126, s63
	v_add3_u32 v233, v233, v127, s63
	v_perm_b32 v242, v227, v226, s64
	v_perm_b32 v243, v229, v228, s64
	v_perm_b32 v244, v231, v230, s64
	v_perm_b32 v245, v233, v232, s64
	s_nop 0
	global_store_dwordx4 v85, v[242:245], s[6:7]
	ds_read_b32 v226, v118
	ds_read_b32 v227, v118 offset:512
	ds_read_b32 v228, v118 offset:1024
	ds_read_b32 v229, v118 offset:1536
	ds_read_b32 v230, v118 offset:2048
	ds_read_b32 v231, v118 offset:2560
	ds_read_b32 v232, v118 offset:3072
	ds_read_b32 v233, v118 offset:3584
	s_waitcnt lgkmcnt(0)
	v_bfe_u32 v120, v226, 16, 1
	v_bfe_u32 v121, v227, 16, 1
	v_bfe_u32 v122, v228, 16, 1
	v_bfe_u32 v123, v229, 16, 1
	v_bfe_u32 v124, v230, 16, 1
	v_bfe_u32 v125, v231, 16, 1
	v_bfe_u32 v126, v232, 16, 1
	v_bfe_u32 v127, v233, 16, 1
	v_add3_u32 v226, v226, v120, s63
	v_add3_u32 v227, v227, v121, s63
	v_add3_u32 v228, v228, v122, s63
	v_add3_u32 v229, v229, v123, s63
	v_add3_u32 v230, v230, v124, s63
	v_add3_u32 v231, v231, v125, s63
	v_add3_u32 v232, v232, v126, s63
	v_add3_u32 v233, v233, v127, s63
	v_perm_b32 v242, v227, v226, s64
	v_perm_b32 v243, v229, v228, s64
	v_perm_b32 v244, v231, v230, s64
	v_perm_b32 v245, v233, v232, s64
	s_nop 0
	global_store_dwordx4 v86, v[242:245], s[6:7]
	s_waitcnt vmcnt(8)
	v_mul_f32_e32 v176, v58, v176
	v_mul_f32_e32 v177, v58, v177
	v_mul_f32_e32 v178, v58, v178
	v_mul_f32_e32 v179, v58, v179
	ds_write_b128 v210, v[176:179]
	v_mul_f32_e32 v180, v59, v180
	v_mul_f32_e32 v181, v59, v181
	v_mul_f32_e32 v182, v59, v182
	v_mul_f32_e32 v183, v59, v183
	ds_write_b128 v210, v[180:183] offset:1024
	v_mul_f32_e32 v184, v60, v184
	v_mul_f32_e32 v185, v60, v185
	v_mul_f32_e32 v186, v60, v186
	v_mul_f32_e32 v187, v60, v187
	ds_write_b128 v210, v[184:187] offset:2048
	v_mul_f32_e32 v188, v61, v188
	v_mul_f32_e32 v189, v61, v189
	v_mul_f32_e32 v190, v61, v190
	v_mul_f32_e32 v191, v61, v191
	ds_write_b128 v210, v[188:191] offset:3072
	v_mul_f32_e32 v192, v62, v192
	v_mul_f32_e32 v193, v62, v193
	v_mul_f32_e32 v194, v62, v194
	v_mul_f32_e32 v195, v62, v195
	ds_write_b128 v210, v[192:195] offset:4096
	v_mul_f32_e32 v196, v63, v196
	v_mul_f32_e32 v197, v63, v197
	v_mul_f32_e32 v198, v63, v198
	v_mul_f32_e32 v199, v63, v199
	ds_write_b128 v210, v[196:199] offset:5120
	v_mul_f32_e32 v200, v64, v200
	v_mul_f32_e32 v201, v64, v201
	v_mul_f32_e32 v202, v64, v202
	v_mul_f32_e32 v203, v64, v203
	ds_write_b128 v210, v[200:203] offset:6144
	v_mul_f32_e32 v204, v65, v204
	v_mul_f32_e32 v205, v65, v205
	v_mul_f32_e32 v206, v65, v206
	v_mul_f32_e32 v207, v65, v207
	ds_write_b128 v210, v[204:207] offset:7168
	s_waitcnt lgkmcnt(0)
	s_barrier
; #define GAS __attribute__((address_space(1)))
; #define LAS __attribute__((address_space(3)))
; #define LDS_WAIT() asm volatile("s_waitcnt lgkmcnt(0)" ::: "memory")
; __device__ __forceinline__ unsigned pk2(float lo, float hi) { return f2bf(lo) | (f2bf(hi) << 16); }
; __device__ __forceinline__ int nat_dim(int p) { return (p >> 1) + 64 * (p & 1); }
; template <int MAP, bool KS, bool KPERM = false>
; __device__ __forceinline__ void p0_transpose_item(const float* W, int K, int Nsrc, int nblk, bf16* WT, const float* ksA, const float* ksB, int ksplit, LAS float* scr, int item, int lane) {
;     const int kb = item / nblk, nb = item % nblk, k0 = 64 * kb, n0 = 32 * nb;
;     const int nr = n0 + (lane & 31); const int sc = MAP == 1 ? src_col_in(nr) : (MAP == 2 ? nat_dim(nr) : nr);
;     float v[32];
; #pragma unroll
;     for (int i = 0; i < 32; ++i) { const int k = k0 + 2 * i + (lane >> 5); const int ksrc = KPERM ? ((k & ~127) + nat_dim(k & 127)) : k;
;         v[i] = sc >= 0 ? W[(size_t)ksrc * Nsrc + sc] : 0.f; }
; #pragma unroll
;     for (int i = 0; i < 32; ++i) { const int kk = 2 * i + (lane >> 5); const int k = k0 + kk;
;         if (KS) v[i] *= (k < ksplit ? ksA[k] : ksB[k - ksplit]);
;         scr[kk * 33 + (lane & 31)] = v[i]; }
;     LDS_WAIT(); asm volatile("" ::: "memory");
;     const int c = lane & 7;
; #pragma unroll
;     for (int j = 0; j < 4; ++j) { const int n = (lane >> 3) + 8 * j; const LAS float* s = scr + (8 * c) * 33 + n;
;         v4u o; o.x = pk2(s[0 * 33], s[1 * 33]); o.y = pk2(s[2 * 33], s[3 * 33]); o.z = pk2(s[4 * 33], s[5 * 33]); o.w = pk2(s[6 * 33], s[7 * 33]);
;         *(GAS v4u*)(WT + (size_t)(n0 + n) * K + k0 + 8 * c) = o; }
;     LDS_WAIT(); asm volatile("" ::: "memory");
; }
; __global__ void __launch_bounds__(NWAVES * 64, 2) hybrid_fwd(Args args) {
;     ...
;             if (r < I_O) { if (l >= WO_F8_FROM) p0_transpose_item_f8<true>(args.in[13] + (size_t)l * DM * DM, DM, DM, DM / 32, (unsigned char*)(ws + WS_WO + l * SZ_WO), 64.f, args.in[6] + l * 2048, args.in[12] + l * 2048, 2048, scr, r, lane);
;                 else p0_transpose_item<0, true>(args.in[13] + (size_t)l * DM * DM, DM, DM, DM / 32, (bf16*)(ws + WS_WO + l * SZ_WO), args.in[6] + l * 2048, args.in[12] + l * 2048, 2048, scr, r, lane); continue; } r -= I_O;
	s_add_u32 s6, s56, 0x1800000
	s_addc_u32 s7, s57, 0
	ds_read_b32 v226, v113
	ds_read_b32 v227, v113 offset:512
	ds_read_b32 v228, v113 offset:1024
	ds_read_b32 v229, v113 offset:1536
	ds_read_b32 v230, v113 offset:2048
	ds_read_b32 v231, v113 offset:2560
	ds_read_b32 v232, v113 offset:3072
	ds_read_b32 v233, v113 offset:3584
	s_waitcnt lgkmcnt(0)
	v_bfe_u32 v120, v226, 16, 1
	v_bfe_u32 v121, v227, 16, 1
	v_bfe_u32 v122, v228, 16, 1
	v_bfe_u32 v123, v229, 16, 1
	v_bfe_u32 v124, v230, 16, 1
	v_bfe_u32 v125, v231, 16, 1
	v_bfe_u32 v126, v232, 16, 1
	v_bfe_u32 v127, v233, 16, 1
	v_add3_u32 v226, v226, v120, s63
	v_add3_u32 v227, v227, v121, s63
	v_add3_u32 v228, v228, v122, s63
	v_add3_u32 v229, v229, v123, s63
	v_add3_u32 v230, v230, v124, s63
	v_add3_u32 v231, v231, v125, s63
	v_add3_u32 v232, v232, v126, s63
	v_add3_u32 v233, v233, v127, s63
	v_perm_b32 v242, v227, v226, s64
	v_perm_b32 v243, v229, v228, s64
	v_perm_b32 v244, v231, v230, s64
	v_perm_b32 v245, v233, v232, s64
	s_nop 0
	global_store_dwordx4 v83, v[242:245], s[6:7]
	ds_read_b32 v226, v115
	ds_read_b32 v227, v115 offset:512
	ds_read_b32 v228, v115 offset:1024
	ds_read_b32 v229, v115 offset:1536
	ds_read_b32 v230, v115 offset:2048
	ds_read_b32 v231, v115 offset:2560
	ds_read_b32 v232, v115 offset:3072
	ds_read_b32 v233, v115 offset:3584
	s_waitcnt lgkmcnt(0)
	v_bfe_u32 v120, v226, 16, 1
	v_bfe_u32 v121, v227, 16, 1
	v_bfe_u32 v122, v228, 16, 1
	v_bfe_u32 v123, v229, 16, 1
	v_bfe_u32 v124, v230, 16, 1
	v_bfe_u32 v125, v231, 16, 1
	v_bfe_u32 v126, v232, 16, 1
	v_bfe_u32 v127, v233, 16, 1
	v_add3_u32 v226, v226, v120, s63
	v_add3_u32 v227, v227, v121, s63
	v_add3_u32 v228, v228, v122, s63
	v_add3_u32 v229, v229, v123, s63
	v_add3_u32 v230, v230, v124, s63
	v_add3_u32 v231, v231, v125, s63
	v_add3_u32 v232, v232, v126, s63
	v_add3_u32 v233, v233, v127, s63
	v_perm_b32 v242, v227, v226, s64
	v_perm_b32 v243, v229, v228, s64
	v_perm_b32 v244, v231, v230, s64
	v_perm_b32 v245, v233, v232, s64
	s_nop 0
	global_store_dwordx4 v84, v[242:245], s[6:7]
	ds_read_b32 v226, v117
	ds_read_b32 v227, v117 offset:512
	ds_read_b32 v228, v117 offset:1024
	ds_read_b32 v229, v117 offset:1536
	ds_read_b32 v230, v117 offset:2048
	ds_read_b32 v231, v117 offset:2560
	ds_read_b32 v232, v117 offset:3072
	ds_read_b32 v233, v117 offset:3584
	s_waitcnt lgkmcnt(0)
	v_bfe_u32 v120, v226, 16, 1
	v_bfe_u32 v121, v227, 16, 1
	v_bfe_u32 v122, v228, 16, 1
	v_bfe_u32 v123, v229, 16, 1
	v_bfe_u32 v124, v230, 16, 1
	v_bfe_u32 v125, v231, 16, 1
	v_bfe_u32 v126, v232, 16, 1
	v_bfe_u32 v127, v233, 16, 1
	v_add3_u32 v226, v226, v120, s63
	v_add3_u32 v227, v227, v121, s63
	v_add3_u32 v228, v228, v122, s63
	v_add3_u32 v229, v229, v123, s63
	v_add3_u32 v230, v230, v124, s63
	v_add3_u32 v231, v231, v125, s63
	v_add3_u32 v232, v232, v126, s63
	v_add3_u32 v233, v233, v127, s63
	v_perm_b32 v242, v227, v226, s64
	v_perm_b32 v243, v229, v228, s64
	v_perm_b32 v244, v231, v230, s64
	v_perm_b32 v245, v233, v232, s64
	s_nop 0
	global_store_dwordx4 v85, v[242:245], s[6:7]
	ds_read_b32 v226, v119
	ds_read_b32 v227, v119 offset:512
	ds_read_b32 v228, v119 offset:1024
	ds_read_b32 v229, v119 offset:1536
	ds_read_b32 v230, v119 offset:2048
	ds_read_b32 v231, v119 offset:2560
	ds_read_b32 v232, v119 offset:3072
	ds_read_b32 v233, v119 offset:3584
	s_waitcnt lgkmcnt(0)
	v_bfe_u32 v120, v226, 16, 1
	v_bfe_u32 v121, v227, 16, 1
	v_bfe_u32 v122, v228, 16, 1
	v_bfe_u32 v123, v229, 16, 1
	v_bfe_u32 v124, v230, 16, 1
	v_bfe_u32 v125, v231, 16, 1
	v_bfe_u32 v126, v232, 16, 1
	v_bfe_u32 v127, v233, 16, 1
	v_add3_u32 v226, v226, v120, s63
	v_add3_u32 v227, v227, v121, s63
	v_add3_u32 v228, v228, v122, s63
	v_add3_u32 v229, v229, v123, s63
	v_add3_u32 v230, v230, v124, s63
	v_add3_u32 v231, v231, v125, s63
	v_add3_u32 v232, v232, v126, s63
	v_add3_u32 v233, v233, v127, s63
	v_perm_b32 v242, v227, v226, s64
	v_perm_b32 v243, v229, v228, s64
	v_perm_b32 v244, v231, v230, s64
	v_perm_b32 v245, v233, v232, s64
	s_nop 0
	global_store_dwordx4 v86, v[242:245], s[6:7]
	s_waitcnt lgkmcnt(0)
	s_barrier
; __global__ void __launch_bounds__(NWAVES * 64, 2) hybrid_fwd(Args args) {
;     ...
;     for (int L = 0; L < DEPTH; ++L) {
;         { unsigned long long wz = 0; asm volatile("" : "+s"(wz)); ws = args.ws + wz; }
;         bf16* Hres = (bf16*)(ws + WS_H);     static_assert(DEPTH == 2 && WO_F8_FROM == 1 && PROJ_F8_FROM == 1, "the phase instantiations below are written for this precision plan");
;         bf16* XN = (bf16*)(ws + WS_XN); bf16* PROJ = (bf16*)(ws + WS_PROJ); bf16* ACT = (bf16*)(ws + WS_ACT); unsigned char* CAT = (unsigned char*)(ws + WS_CAT);     const bool wo_f8 = L >= WO_F8_FROM;
;         float* ATT = (float*)(ws + WS_ATT); bf16* XBC = (bf16*)(ws + WS_XBC); bf16* Y = (bf16*)(ws + WS_Y);
;         bf16* KC = (bf16*)(ws + WS_KC); bf16* VC = (bf16*)(ws + WS_VC); float* DT = (float*)(ws + WS_DT); float* ADT = (float*)(ws + WS_ADT);
;         float* COS = (float*)(ws + WS_COS); float* SIN = (float*)(ws + WS_SIN); unsigned* BMP = (unsigned*)(ws + WS_BMP);
;         bf16* AO = (bf16*)(ws + WS_ACT);     float* STT = (float*)(ws + WS_ST); bf16* PREVB = (bf16*)(ws + WS_PREV);     float* ACSG = (float*)(ws + WS_ACSG); float* DEC = (float*)(ws + WS_DEC);
;         {
;             const bool split = (L < PROJ_F8_FROM) && (F.G == 256);
;             if (L >= PROJ_F8_FROM) { pg8::StaticOrder So; So.init(S, NPROJ, F.G, (int)blockIdx.x); pg8::Gemm g{XN, (const bf16*)(ws + WS_WIN + L * SZ_WIN), S, NPROJ, DM / 2};
;                 pg8::EpiProj E{PROJ, NPROJ, COS, SIN, QSCALE, 1.f / (XN8_SCALE * WUP8_SCALE), 0};
;                 pg8::gemm_phase<pg8::EpiProj, pg8::StaticOrder, true, true, true>(F.lds + RING_OFF, g, So, E); }
	v_readlane_b32 s12, v253, 35
	v_readlane_b32 s18, v253, 41
	v_readlane_b32 s19, v253, 42
	s_add_u32 s81, s18, 0x1f600000
	s_addc_u32 s94, s19, 0
	s_add_u32 s24, s18, 0xf600000
	v_or_b32_e32 v2, 2, v6
	v_mov_b32_e32 v3, 0x630
	v_readlane_b32 s13, v253, 36
	v_readlane_b32 s14, v253, 37
	v_readlane_b32 s15, v253, 38
	s_addc_u32 s25, s19, 0
	v_mad_u32_u24 v58, v2, s0, v3
	v_mov_b32_e32 v3, 0xc60
	s_add_u32 s26, s18, 0xb600000
	v_mad_u32_u24 v59, v2, s0, v3
	v_readlane_b32 s0, v253, 19
	s_addc_u32 s27, s19, 0
	v_readlane_b32 s2, v253, 21
	v_readlane_b32 s10, v253, 29
	v_readlane_b32 s3, v253, 22
	v_readlane_b32 s11, v253, 30
	s_add_u32 s2, s10, 0x4000000
	v_readlane_b32 s40, v253, 3
	s_addc_u32 s3, s11, 0
	v_readlane_b32 s52, v253, 15
	v_readlane_b32 s53, v253, 16
	s_add_u32 s22, s52, 0x2000
	v_readlane_b32 s8, v253, 27
	s_addc_u32 s23, s53, 0
	v_readlane_b32 s9, v253, 28
	s_add_u32 s84, s8, 0x2000
	s_addc_u32 s85, s9, 0
	s_add_u32 s33, s18, 0x200000
	v_readlane_b32 s44, v253, 7
	s_addc_u32 s38, s19, 0
	v_mov_b32_e32 v9, v11
	v_readlane_b32 s1, v253, 20
	v_readlane_b32 s45, v253, 8
	s_add_u32 s86, s44, 0xb140000
	v_mul_u32_u24_e32 v57, 0x84, v2
	v_readlane_b32 s42, v253, 5
	v_lshl_add_u64 v[2:3], s[18:19], 0, v[8:9]
	s_mov_b64 s[0:1], 0xd600000
	s_addc_u32 s87, s45, 0
	v_readlane_b32 s12, v253, 31
	v_readlane_b32 s13, v253, 32
	v_readlane_b32 s14, v253, 33
	v_readlane_b32 s15, v253, 34
	v_readlane_b32 s43, v253, 6
	v_readlane_b32 s54, v253, 17
	v_readlane_b32 s55, v253, 18
	v_lshl_add_u64 v[12:13], v[2:3], 0, s[0:1]
	s_add_u32 s88, s42, 0x4000
	s_mov_b64 s[0:1], 0x5c00000
	v_readlane_b32 s41, v253, 4
	v_readlane_b32 s46, v253, 9
	v_readlane_b32 s47, v253, 10
	v_readlane_b32 s48, v253, 11
	v_readlane_b32 s49, v253, 12
	v_readlane_b32 s50, v253, 13
	s_addc_u32 s89, s43, 0
	v_lshlrev_b32_e32 v4, 6, v18
	v_lshl_add_u64 v[14:15], v[2:3], 0, s[0:1]
	s_lshl_b32 s0, s80, 5
	s_movk_i32 s12, 0xe000
	s_movk_i32 s14, 0xe008
	s_movk_i32 s18, 0xe010
	s_movk_i32 s78, 0xe018
	s_movk_i32 s92, 0xe0d0
	s_movk_i32 s28, 0xe0d8
	s_movk_i32 s34, 0xe0e0
	s_movk_i32 s52, 0xe0e8
	s_movk_i32 s54, 0xe0f0
	s_movk_i32 s56, 0xe0f8
	v_or_b32_e32 v26, 0x2000, v18
	v_or_b32_e32 v27, 0x4000, v18
	v_or_b32_e32 v28, 0x6000, v18
	v_or_b32_e32 v29, 0x8000, v18
	v_or_b32_e32 v30, 0xa000, v18
	v_or_b32_e32 v31, 0xc000, v18
	v_or_b32_e32 v32, 0xe000, v18
	v_or_b32_e32 v33, 0x10000, v18
	v_or_b32_e32 v34, 0x12000, v18
	v_or_b32_e32 v35, 0x14000, v18
	v_or_b32_e32 v36, 0x16000, v18
	v_or_b32_e32 v37, 0x18000, v18
	v_or_b32_e32 v38, 0x1a000, v18
	v_or_b32_e32 v39, 0x1c000, v18
	v_or_b32_e32 v40, 0x1e000, v18
	v_or_b32_e32 v41, 0x20000, v18
	v_or_b32_e32 v42, 0x22000, v18
	v_or_b32_e32 v43, 0x24000, v18
	v_or_b32_e32 v44, 0x26000, v18
	v_or_b32_e32 v45, 0x28000, v18
	v_or_b32_e32 v46, 0x2a000, v18
	v_or_b32_e32 v47, 0x2c000, v18
	v_or_b32_e32 v48, 0x2e000, v18
	v_or_b32_e32 v49, 0x30000, v18
	v_or_b32_e32 v50, 0x32000, v18
	v_or_b32_e32 v51, 0x34000, v18
	v_or_b32_e32 v52, 0x36000, v18
	v_or_b32_e32 v53, 0x38000, v18
	v_or_b32_e32 v54, 0x3a000, v18
	v_or_b32_e32 v55, 0x3c000, v18
	v_or_b32_e32 v56, 0x3e000, v18
	v_and_b32_e32 v60, 64, v4
	v_mov_b32_e32 v7, v11
	s_lshl_b32 s39, s80, 6
	s_add_i32 s40, s0, 0xfff4c000
	s_lshl_b32 s41, s83, 8
	s_lshl_b32 s42, s80, 4
	s_lshl_b32 s43, s83, 7
	s_mov_b32 s91, 0
	s_mov_b32 s44, 0xc3e00000
	s_movk_i32 s45, 0x7fff
	s_mov_b32 s46, 0xffff0000
	s_movk_i32 s47, 0x2c2f
	s_movk_i32 s48, 0x2c50
	s_mov_b32 s49, 0xb140
	v_add_u32_e32 v61, 0x400, v19
	v_add_u32_e32 v62, 0x800, v19
	v_add_u32_e32 v63, 0xc00, v19
	v_mov_b32_e32 v64, 0x43e00000
	s_mov_b32 s50, s80
	s_mov_b32 s13, -1
	s_mov_b32 s15, -1
	s_mov_b32 s19, -1
	s_mov_b32 s79, -1
	s_mov_b32 s93, -1
	s_mov_b32 s29, -1
	s_mov_b32 s35, -1
	s_mov_b32 s53, -1
	s_mov_b32 s55, -1
	s_mov_b32 s57, -1
	v_readlane_b32 s16, v253, 39
	v_readlane_b32 s17, v253, 40
	v_readlane_b32 s4, v253, 23
	v_readlane_b32 s5, v253, 24
	v_readlane_b32 s6, v253, 25
	v_readlane_b32 s7, v253, 26
	v_readlane_b32 s51, v253, 14
	s_branch .LBB0_15

; #define GAS __attribute__((address_space(1)))
; #define LAS __attribute__((address_space(3)))
; #define LDS_WAIT() asm volatile("s_waitcnt lgkmcnt(0)" ::: "memory")
;     const int pr = item >> 1, kb = 2 * (pr / nblk) + (item & 1), nb = pr % nblk, k0 = 64 * kb, n0 = 32 * nb;
;     const int nr = n0 + (lane & 31); const int sc = MAP == 1 ? src_col_in(nr) : nr;
;     float v[32];
; #pragma unroll
;     for (int i = 0; i < 32; ++i) v[i] = sc >= 0 ? W[(size_t)(k0 + 2 * i + (lane >> 5)) * Nsrc + sc] : 0.f;
; #pragma unroll
;     for (int i = 0; i < 32; ++i) { const int k = k0 + 2 * i + (lane >> 5); float x = v[i] * wscale; if (KS) x *= (k < ksplit ? ksA[k] : ksB[k - ksplit]); scr[(2 * i + (lane >> 5)) * 33 + (lane & 31)] = x; }
;     LDS_WAIT(); asm volatile("" ::: "memory");
;     const int c = lane & 7;
; #pragma unroll
;     for (int j = 0; j < 4; ++j) { const int n = (lane >> 3) + 8 * j; const LAS float* s = scr + (8 * c) * 33 + n;
;         const unsigned long long o = (unsigned long long)pg8::pk4_fp8(s[0 * 33], s[1 * 33], s[2 * 33], s[3 * 33]) | ((unsigned long long)pg8::pk4_fp8(s[4 * 33], s[5 * 33], s[6 * 33], s[7 * 33]) << 32);
;         *(GAS unsigned long long*)(WT + (size_t)(n0 + n) * K + k0 + 8 * c) = o; }
;     LDS_WAIT(); asm volatile("" ::: "memory");
; __global__ void __launch_bounds__(NWAVES * 64, 2) hybrid_fwd(Args args) {
;     ...
;             if (r < I_O) { if (l >= WO_F8_FROM) p0_transpose_item_f8<true>(args.in[13] + (size_t)l * DM * DM, DM, DM, DM / 32, (unsigned char*)(ws + WS_WO + l * SZ_WO), 64.f, args.in[6] + l * 2048, args.in[12] + l * 2048, 2048, scr, r, lane);
;                 else p0_transpose_item<0, true>(args.in[13] + (size_t)l * DM * DM, DM, DM, DM / 32, (bf16*)(ws + WS_WO + l * SZ_WO), args.in[6] + l * 2048, args.in[12] + l * 2048, 2048, scr, r, lane); continue; } r -= I_O;
;             if (r < I_UP) { p0_transpose_item_f8<true>(args.in[15] + (size_t)l * DM * FF, DM, FF, FF / 32, (unsigned char*)(ws + WS_WUP + l * SZ_WUP), WUP8_SCALE, args.in[14] + l * DM, args.in[14] + l * DM, DM, scr, r, lane); continue; } r -= I_UP;
;             p0_transpose_item_f8<false>(args.in[16] + (size_t)l * FF * DM, FF, DM, DM / 32, (unsigned char*)(ws + WS_WDN + l * SZ_WDN), 128.f, args.in[16], args.in[16], 0, scr, r, lane);
.LBB0_575:
	s_waitcnt vmcnt(0)
	s_barrier
	s_cmpk_lt_u32 s77, 0xa0
	s_cbranch_scc1 .Llite_skip
	s_sub_i32 s16, s77, 160
	v_and_b32_e32 v17, 63, v0
	v_lshrrev_b32_e32 v18, 6, v0
	v_lshrrev_b32_e32 v14, 5, v17
	v_lshl_add_u32 v15, v18, 4, v14
	v_and_b32_e32 v16, 31, v17
	v_xor_b32_e32 v16, v16, v18
	v_lshlrev_b32_e32 v16, 4, v16
	v_lshl_add_u32 v4, v15, 9, v16
	v_add_u32_e32 v5, 0x10000, v4
	v_and_b32_e32 v16, 31, v17
	v_lshlrev_b32_e32 v16, 4, v16
	s_mov_b32 s21, 0x4000
	v_mad_u32_u24 v10, v15, s21, v16
	v_and_b32_e32 v14, 7, v17
	v_lshrrev_b32_e32 v15, 5, v17
	v_lshl_add_u32 v15, v18, 2, v15
	v_xor_b32_e32 v15, v15, v14
	v_lshlrev_b32_e32 v15, 4, v15
	v_lshl_add_u32 v15, v14, 13, v15
	v_bfe_u32 v16, v17, 3, 2
	v_lshl_add_u32 v6, v16, 2, v15
	v_add_u32_e32 v7, 0x10000, v6
	v_and_b32_e32 v14, 7, v17
	v_lshrrev_b32_e32 v15, 5, v17
	v_lshl_add_u32 v15, v18, 2, v15
	v_add_u32_e32 v15, 2, v15
	v_xor_b32_e32 v15, v15, v14
	v_lshlrev_b32_e32 v15, 4, v15
	v_lshl_add_u32 v15, v14, 13, v15
	v_bfe_u32 v16, v17, 3, 2
	v_lshl_add_u32 v8, v16, 2, v15
	v_add_u32_e32 v9, 0x10000, v8
	v_lshrrev_b32_e32 v14, 3, v17
	v_lshl_add_u32 v14, v18, 4, v14
	v_and_b32_e32 v15, 7, v17
	v_lshlrev_b32_e32 v15, 4, v15
	v_lshl_add_u32 v11, v14, 14, v15
	v_lshrrev_b32_e32 v14, 3, v17
	v_lshl_add_u32 v14, v18, 4, v14
	v_add_u32_e32 v14, 8, v14
	v_and_b32_e32 v15, 7, v17
	v_lshlrev_b32_e32 v15, 4, v15
	v_lshl_add_u32 v12, v14, 14, v15
	v_mov_b32_e32 v13, 0x43e00000
	s_mov_b32 s20, 0xc3e00000
	v_readlane_b32 s2, v253, 35
	v_readlane_b32 s3, v253, 36
	v_readlane_b32 s4, v253, 41
	v_readlane_b32 s5, v253, 42
	s_add_u32 s2, s2, 0x10000000
	s_addc_u32 s3, s3, 0
	s_add_u32 s4, s4, 0x27600000
	s_addc_u32 s5, s5, 0
	s_and_b32 s38, s16, 31
	s_lshr_b32 s39, s16, 5
	v_lshrrev_b32_e32 v14, 5, v17
	v_lshl_add_u32 v15, v18, 4, v14
	v_lshlrev_b32_e32 v19, 2, v15
	v_lshrrev_b32_e32 v14, 3, v17
	v_lshl_add_u32 v14, v18, 4, v14
	v_and_b32_e32 v15, 7, v17
	v_lshlrev_b32_e32 v15, 4, v15
	v_lshl_add_u32 v28, v14, 12, v15
	v_lshrrev_b32_e32 v14, 3, v17
	v_lshl_add_u32 v14, v18, 4, v14
	v_add_u32_e32 v14, 8, v14
	v_and_b32_e32 v15, 7, v17
	v_lshlrev_b32_e32 v15, 4, v15
	v_lshl_add_u32 v29, v14, 12, v15
	v_readlane_b32 s0, v253, 15
	v_readlane_b32 s1, v253, 16
	v_readlane_b32 s22, v253, 27
	v_readlane_b32 s23, v253, 28
	s_sub_i32 s45, s38, 16
	s_cmp_lt_u32 s38, 16
	s_cselect_b32 s0, s0, s22
	s_cselect_b32 s1, s1, s23
	s_cselect_b32 s45, s38, s45
	s_lshl_b32 s45, s45, 9
	s_add_i32 s45, s45, 0x2000
	s_add_u32 s0, s0, s45
	s_addc_u32 s1, s1, 0
	global_load_dword v20, v19, s[0:1] offset:0
	global_load_dword v21, v19, s[0:1] offset:8
	global_load_dword v22, v19, s[0:1] offset:16
	global_load_dword v23, v19, s[0:1] offset:24
	global_load_dword v24, v19, s[0:1] offset:32
	global_load_dword v25, v19, s[0:1] offset:40
	global_load_dword v26, v19, s[0:1] offset:48
	global_load_dword v27, v19, s[0:1] offset:56
	s_waitcnt vmcnt(0)
	v_mul_f32_e32 v20, 0x42800000, v20
	v_mul_f32_e32 v21, 0x42800000, v21
	v_mul_f32_e32 v22, 0x42800000, v22
	v_mul_f32_e32 v23, 0x42800000, v23
	v_mul_f32_e32 v24, 0x42800000, v24
	v_mul_f32_e32 v25, 0x42800000, v25
	v_mul_f32_e32 v26, 0x42800000, v26
	v_mul_f32_e32 v27, 0x42800000, v27
	v_readlane_b32 s22, v253, 29
	v_readlane_b32 s23, v253, 30
	s_add_u32 s22, s22, 0x4000000
	s_addc_u32 s23, s23, 0
	s_lshl_b32 s45, s38, 21
	s_add_u32 s22, s22, s45
	s_addc_u32 s23, s23, 0
	v_readlane_b32 s50, v253, 41
	v_readlane_b32 s51, v253, 42
	s_add_u32 s50, s50, 0xd600000
	s_addc_u32 s51, s51, 0
	s_lshl_b32 s45, s38, 7
	s_add_u32 s50, s50, s45
	s_addc_u32 s51, s51, 0
	s_add_i32 s17, s16, 0
	s_min_u32 s17, s17, 0xfff
	s_lshr_b32 s18, s17, 5
	s_add_i32 s18, s18, 0
	s_and_b32 s19, s17, 31
	s_lshl_b32 s18, s18, 21
	s_lshl_b32 s19, s19, 9
	s_add_u32 s18, s18, s19
	s_add_u32 s12, s2, s18
	s_addc_u32 s13, s3, 0
	global_load_dwordx4 v[36:39], v10, s[12:13]
	s_add_u32 s12, s12, 0x8000
	s_addc_u32 s13, s13, 0
	global_load_dwordx4 v[40:43], v10, s[12:13]
	s_add_u32 s12, s12, 0x8000
	s_addc_u32 s13, s13, 0
	global_load_dwordx4 v[44:47], v10, s[12:13]
	s_add_u32 s12, s12, 0x8000
	s_addc_u32 s13, s13, 0
	global_load_dwordx4 v[48:51], v10, s[12:13]
	s_add_u32 s12, s12, 0x8000
	s_addc_u32 s13, s13, 0
	global_load_dwordx4 v[52:55], v10, s[12:13]
	s_add_u32 s12, s12, 0x8000
	s_addc_u32 s13, s13, 0
	global_load_dwordx4 v[56:59], v10, s[12:13]
	s_add_u32 s12, s12, 0x8000
	s_addc_u32 s13, s13, 0
	global_load_dwordx4 v[60:63], v10, s[12:13]
	s_add_u32 s12, s12, 0x8000
	s_addc_u32 s13, s13, 0
	global_load_dwordx4 v[64:67], v10, s[12:13]
	s_add_i32 s17, s16, 96
	s_min_u32 s17, s17, 0xfff
	s_lshr_b32 s18, s17, 5
	s_add_i32 s18, s18, 0
	s_and_b32 s19, s17, 31
	s_lshl_b32 s18, s18, 21
	s_lshl_b32 s19, s19, 9
	s_add_u32 s18, s18, s19
	s_add_u32 s12, s2, s18
	s_addc_u32 s13, s3, 0
	global_load_dwordx4 v[68:71], v10, s[12:13]
	s_add_u32 s12, s12, 0x8000
	s_addc_u32 s13, s13, 0
	global_load_dwordx4 v[72:75], v10, s[12:13]
	s_add_u32 s12, s12, 0x8000
	s_addc_u32 s13, s13, 0
	global_load_dwordx4 v[76:79], v10, s[12:13]
	s_add_u32 s12, s12, 0x8000
	s_addc_u32 s13, s13, 0
	global_load_dwordx4 v[80:83], v10, s[12:13]
	s_add_u32 s12, s12, 0x8000
	s_addc_u32 s13, s13, 0
	global_load_dwordx4 v[84:87], v10, s[12:13]
	s_add_u32 s12, s12, 0x8000
	s_addc_u32 s13, s13, 0
	global_load_dwordx4 v[88:91], v10, s[12:13]
	s_add_u32 s12, s12, 0x8000
	s_addc_u32 s13, s13, 0
	global_load_dwordx4 v[92:95], v10, s[12:13]
	s_add_u32 s12, s12, 0x8000
	s_addc_u32 s13, s13, 0
	global_load_dwordx4 v[96:99], v10, s[12:13]
	s_add_i32 s17, s16, 192
	s_min_u32 s17, s17, 0xfff
	s_lshr_b32 s18, s17, 5
	s_add_i32 s18, s18, 0
	s_and_b32 s19, s17, 31
; #define GAS __attribute__((address_space(1)))
; #define LAS __attribute__((address_space(3)))
; #define LDS_WAIT() asm volatile("s_waitcnt lgkmcnt(0)" ::: "memory")
;     const int pr = item >> 1, kb = 2 * (pr / nblk) + (item & 1), nb = pr % nblk, k0 = 64 * kb, n0 = 32 * nb;
;     const int nr = n0 + (lane & 31); const int sc = MAP == 1 ? src_col_in(nr) : nr;
;     float v[32];
; #pragma unroll
;     for (int i = 0; i < 32; ++i) v[i] = sc >= 0 ? W[(size_t)(k0 + 2 * i + (lane >> 5)) * Nsrc + sc] : 0.f;
; #pragma unroll
;     for (int i = 0; i < 32; ++i) { const int k = k0 + 2 * i + (lane >> 5); float x = v[i] * wscale; if (KS) x *= (k < ksplit ? ksA[k] : ksB[k - ksplit]); scr[(2 * i + (lane >> 5)) * 33 + (lane & 31)] = x; }
;     LDS_WAIT(); asm volatile("" ::: "memory");
;     const int c = lane & 7;
; #pragma unroll
;     for (int j = 0; j < 4; ++j) { const int n = (lane >> 3) + 8 * j; const LAS float* s = scr + (8 * c) * 33 + n;
;         const unsigned long long o = (unsigned long long)pg8::pk4_fp8(s[0 * 33], s[1 * 33], s[2 * 33], s[3 * 33]) | ((unsigned long long)pg8::pk4_fp8(s[4 * 33], s[5 * 33], s[6 * 33], s[7 * 33]) << 32);
;         *(GAS unsigned long long*)(WT + (size_t)(n0 + n) * K + k0 + 8 * c) = o; }
;     LDS_WAIT(); asm volatile("" ::: "memory");
; __global__ void __launch_bounds__(NWAVES * 64, 2) hybrid_fwd(Args args) {
;     ...
;             p0_transpose_item_f8<false>(args.in[16] + (size_t)l * FF * DM, FF, DM, DM / 32, (unsigned char*)(ws + WS_WDN + l * SZ_WDN), 128.f, args.in[16], args.in[16], 0, scr, r, lane);
	s_lshl_b32 s18, s18, 21
	s_lshl_b32 s19, s19, 9
	s_add_u32 s18, s18, s19
	s_add_u32 s12, s2, s18
	s_addc_u32 s13, s3, 0
	global_load_dwordx4 v[100:103], v10, s[12:13]
	s_add_u32 s12, s12, 0x8000
	s_addc_u32 s13, s13, 0
	global_load_dwordx4 v[104:107], v10, s[12:13]
	s_add_u32 s12, s12, 0x8000
	s_addc_u32 s13, s13, 0
	global_load_dwordx4 v[108:111], v10, s[12:13]
	s_add_u32 s12, s12, 0x8000
	s_addc_u32 s13, s13, 0
	global_load_dwordx4 v[112:115], v10, s[12:13]
	s_add_u32 s12, s12, 0x8000
	s_addc_u32 s13, s13, 0
	global_load_dwordx4 v[116:119], v10, s[12:13]
	s_add_u32 s12, s12, 0x8000
	s_addc_u32 s13, s13, 0
	global_load_dwordx4 v[120:123], v10, s[12:13]
	s_add_u32 s12, s12, 0x8000
	s_addc_u32 s13, s13, 0
	global_load_dwordx4 v[124:127], v10, s[12:13]
	s_add_u32 s12, s12, 0x8000
	s_addc_u32 s13, s13, 0
	global_load_dwordx4 v[128:131], v10, s[12:13]
	s_add_i32 s17, s16, 288
	s_min_u32 s17, s17, 0xfff
	s_lshr_b32 s18, s17, 5
	s_add_i32 s18, s18, 0
	s_and_b32 s19, s17, 31
	s_lshl_b32 s18, s18, 21
	s_lshl_b32 s19, s19, 9
	s_add_u32 s18, s18, s19
	s_add_u32 s12, s2, s18
	s_addc_u32 s13, s3, 0
	global_load_dwordx4 v[132:135], v10, s[12:13]
	s_add_u32 s12, s12, 0x8000
	s_addc_u32 s13, s13, 0
	global_load_dwordx4 v[136:139], v10, s[12:13]
	s_add_u32 s12, s12, 0x8000
	s_addc_u32 s13, s13, 0
	global_load_dwordx4 v[140:143], v10, s[12:13]
	s_add_u32 s12, s12, 0x8000
	s_addc_u32 s13, s13, 0
	global_load_dwordx4 v[144:147], v10, s[12:13]
	s_add_u32 s12, s12, 0x8000
	s_addc_u32 s13, s13, 0
	global_load_dwordx4 v[148:151], v10, s[12:13]
	s_add_u32 s12, s12, 0x8000
	s_addc_u32 s13, s13, 0
	global_load_dwordx4 v[152:155], v10, s[12:13]
	s_add_u32 s12, s12, 0x8000
	s_addc_u32 s13, s13, 0
	global_load_dwordx4 v[156:159], v10, s[12:13]
	s_add_u32 s12, s12, 0x8000
	s_addc_u32 s13, s13, 0
	global_load_dwordx4 v[160:163], v10, s[12:13]
	s_waitcnt vmcnt(24)
	v_mul_f32_e32 v36, 0x43000000, v36
	v_mul_f32_e32 v37, 0x43000000, v37
	v_mul_f32_e32 v38, 0x43000000, v38
	v_mul_f32_e32 v39, 0x43000000, v39
	ds_write_b128 v4, v[36:39]
	v_mul_f32_e32 v40, 0x43000000, v40
	v_mul_f32_e32 v41, 0x43000000, v41
	v_mul_f32_e32 v42, 0x43000000, v42
	v_mul_f32_e32 v43, 0x43000000, v43
	ds_write_b128 v4, v[40:43] offset:1024
	v_mul_f32_e32 v44, 0x43000000, v44
	v_mul_f32_e32 v45, 0x43000000, v45
	v_mul_f32_e32 v46, 0x43000000, v46
	v_mul_f32_e32 v47, 0x43000000, v47
	ds_write_b128 v4, v[44:47] offset:2048
	v_mul_f32_e32 v48, 0x43000000, v48
	v_mul_f32_e32 v49, 0x43000000, v49
	v_mul_f32_e32 v50, 0x43000000, v50
	v_mul_f32_e32 v51, 0x43000000, v51
	ds_write_b128 v4, v[48:51] offset:3072
	v_mul_f32_e32 v52, 0x43000000, v52
	v_mul_f32_e32 v53, 0x43000000, v53
	v_mul_f32_e32 v54, 0x43000000, v54
	v_mul_f32_e32 v55, 0x43000000, v55
	ds_write_b128 v4, v[52:55] offset:4096
	v_mul_f32_e32 v56, 0x43000000, v56
	v_mul_f32_e32 v57, 0x43000000, v57
	v_mul_f32_e32 v58, 0x43000000, v58
	v_mul_f32_e32 v59, 0x43000000, v59
	ds_write_b128 v4, v[56:59] offset:5120
	v_mul_f32_e32 v60, 0x43000000, v60
	v_mul_f32_e32 v61, 0x43000000, v61
	v_mul_f32_e32 v62, 0x43000000, v62
	v_mul_f32_e32 v63, 0x43000000, v63
	ds_write_b128 v4, v[60:63] offset:6144
	v_mul_f32_e32 v64, 0x43000000, v64
	v_mul_f32_e32 v65, 0x43000000, v65
	v_mul_f32_e32 v66, 0x43000000, v66
	v_mul_f32_e32 v67, 0x43000000, v67
	ds_write_b128 v4, v[64:67] offset:7168
	s_waitcnt lgkmcnt(0)
	s_barrier
	s_add_i32 s17, s16, 384
	s_min_u32 s17, s17, 0xfff
	s_lshr_b32 s18, s17, 5
	s_add_i32 s18, s18, 0
	s_and_b32 s19, s17, 31
	s_lshl_b32 s18, s18, 21
	s_lshl_b32 s19, s19, 9
	s_add_u32 s18, s18, s19
	s_add_u32 s12, s2, s18
	s_addc_u32 s13, s3, 0
	global_load_dwordx4 v[36:39], v10, s[12:13]
	s_add_u32 s12, s12, 0x8000
	s_addc_u32 s13, s13, 0
	global_load_dwordx4 v[40:43], v10, s[12:13]
	s_add_u32 s12, s12, 0x8000
	s_addc_u32 s13, s13, 0
	global_load_dwordx4 v[44:47], v10, s[12:13]
	s_add_u32 s12, s12, 0x8000
	s_addc_u32 s13, s13, 0
	global_load_dwordx4 v[48:51], v10, s[12:13]
	s_add_u32 s12, s12, 0x8000
	s_addc_u32 s13, s13, 0
	global_load_dwordx4 v[52:55], v10, s[12:13]
	s_add_u32 s12, s12, 0x8000
	s_addc_u32 s13, s13, 0
	global_load_dwordx4 v[56:59], v10, s[12:13]
	s_add_u32 s12, s12, 0x8000
	s_addc_u32 s13, s13, 0
	global_load_dwordx4 v[60:63], v10, s[12:13]
	s_add_u32 s12, s12, 0x8000
	s_addc_u32 s13, s13, 0
	global_load_dwordx4 v[64:67], v10, s[12:13]
	s_add_i32 s17, s16, 0
	s_min_u32 s17, s17, 0xfff
	s_lshr_b32 s18, s17, 5
	s_add_i32 s18, s18, 0
	s_and_b32 s19, s17, 31
	s_lshl_b32 s19, s19, 21
	s_lshl_b32 s18, s18, 7
	s_add_u32 s18, s18, s19
	s_add_u32 s14, s4, s18
	s_addc_u32 s15, s5, 0
	ds_read_b32 v170, v6
	ds_read_b32 v171, v6 offset:512
	ds_read_b32 v172, v6 offset:1024
	ds_read_b32 v173, v6 offset:1536
	ds_read_b32 v174, v6 offset:2048
	ds_read_b32 v175, v6 offset:2560
	ds_read_b32 v176, v6 offset:3072
	ds_read_b32 v177, v6 offset:3584
	ds_read_b32 v196, v6 offset:4096
	ds_read_b32 v197, v6 offset:4608
	ds_read_b32 v198, v6 offset:5120
	ds_read_b32 v199, v6 offset:5632
	ds_read_b32 v200, v6 offset:6144
	ds_read_b32 v201, v6 offset:6656
	ds_read_b32 v202, v6 offset:7168
	ds_read_b32 v203, v6 offset:7680
	s_waitcnt lgkmcnt(0)
; #define GAS __attribute__((address_space(1)))
; #define LAS __attribute__((address_space(3)))
; #define LDS_WAIT() asm volatile("s_waitcnt lgkmcnt(0)" ::: "memory")
;     const int pr = item >> 1, kb = 2 * (pr / nblk) + (item & 1), nb = pr % nblk, k0 = 64 * kb, n0 = 32 * nb;
;     const int nr = n0 + (lane & 31); const int sc = MAP == 1 ? src_col_in(nr) : nr;
;     float v[32];
; #pragma unroll
;     for (int i = 0; i < 32; ++i) v[i] = sc >= 0 ? W[(size_t)(k0 + 2 * i + (lane >> 5)) * Nsrc + sc] : 0.f;
; #pragma unroll
;     for (int i = 0; i < 32; ++i) { const int k = k0 + 2 * i + (lane >> 5); float x = v[i] * wscale; if (KS) x *= (k < ksplit ? ksA[k] : ksB[k - ksplit]); scr[(2 * i + (lane >> 5)) * 33 + (lane & 31)] = x; }
;     LDS_WAIT(); asm volatile("" ::: "memory");
;     const int c = lane & 7;
; #pragma unroll
;     for (int j = 0; j < 4; ++j) { const int n = (lane >> 3) + 8 * j; const LAS float* s = scr + (8 * c) * 33 + n;
;         const unsigned long long o = (unsigned long long)pg8::pk4_fp8(s[0 * 33], s[1 * 33], s[2 * 33], s[3 * 33]) | ((unsigned long long)pg8::pk4_fp8(s[4 * 33], s[5 * 33], s[6 * 33], s[7 * 33]) << 32);
;         *(GAS unsigned long long*)(WT + (size_t)(n0 + n) * K + k0 + 8 * c) = o; }
;     LDS_WAIT(); asm volatile("" ::: "memory");
; __global__ void __launch_bounds__(NWAVES * 64, 2) hybrid_fwd(Args args) {
;     ...
;             p0_transpose_item_f8<false>(args.in[16] + (size_t)l * FF * DM, FF, DM, DM / 32, (unsigned char*)(ws + WS_WDN + l * SZ_WDN), 128.f, args.in[16], args.in[16], 0, scr, r, lane);
	v_max_f32_e32 v170, v170, v170
	v_max_f32_e32 v171, v171, v171
	v_max_f32_e32 v172, v172, v172
	v_max_f32_e32 v173, v173, v173
	v_max_f32_e32 v174, v174, v174
	v_max_f32_e32 v175, v175, v175
	v_max_f32_e32 v176, v176, v176
	v_max_f32_e32 v177, v177, v177
	v_max_f32_e32 v196, v196, v196
	v_max_f32_e32 v197, v197, v197
	v_max_f32_e32 v198, v198, v198
	v_max_f32_e32 v199, v199, v199
	v_max_f32_e32 v200, v200, v200
	v_max_f32_e32 v201, v201, v201
	v_max_f32_e32 v202, v202, v202
	v_max_f32_e32 v203, v203, v203
	v_med3_f32 v170, v170, s20, v13
	v_med3_f32 v171, v171, s20, v13
	v_med3_f32 v172, v172, s20, v13
	v_med3_f32 v173, v173, s20, v13
	v_med3_f32 v174, v174, s20, v13
	v_med3_f32 v175, v175, s20, v13
	v_med3_f32 v176, v176, s20, v13
	v_med3_f32 v177, v177, s20, v13
	v_med3_f32 v196, v196, s20, v13
	v_med3_f32 v197, v197, s20, v13
	v_med3_f32 v198, v198, s20, v13
	v_med3_f32 v199, v199, s20, v13
	v_med3_f32 v200, v200, s20, v13
	v_med3_f32 v201, v201, s20, v13
	v_med3_f32 v202, v202, s20, v13
	v_med3_f32 v203, v203, s20, v13
	v_mov_b32_e32 v208, 0
	v_mov_b32_e32 v209, 0
	v_mov_b32_e32 v210, 0
	v_mov_b32_e32 v211, 0
	v_cvt_pk_fp8_f32 v208, v170, v171
	v_cvt_pk_fp8_f32 v209, v174, v175
	v_cvt_pk_fp8_f32 v210, v196, v197
	v_cvt_pk_fp8_f32 v211, v200, v201
	v_cvt_pk_fp8_f32 v208, v172, v173 op_sel:[0,0,1]
	v_cvt_pk_fp8_f32 v209, v176, v177 op_sel:[0,0,1]
	v_cvt_pk_fp8_f32 v210, v198, v199 op_sel:[0,0,1]
	v_cvt_pk_fp8_f32 v211, v202, v203 op_sel:[0,0,1]
	s_nop 0
	global_store_dwordx4 v11, v[208:211], s[14:15]
	ds_read_b32 v170, v8
	ds_read_b32 v171, v8 offset:512
	ds_read_b32 v172, v8 offset:1024
	ds_read_b32 v173, v8 offset:1536
	ds_read_b32 v174, v8 offset:2048
	ds_read_b32 v175, v8 offset:2560
	ds_read_b32 v176, v8 offset:3072
	ds_read_b32 v177, v8 offset:3584
	ds_read_b32 v196, v8 offset:4096
	ds_read_b32 v197, v8 offset:4608
	ds_read_b32 v198, v8 offset:5120
	ds_read_b32 v199, v8 offset:5632
	ds_read_b32 v200, v8 offset:6144
	ds_read_b32 v201, v8 offset:6656
	ds_read_b32 v202, v8 offset:7168
	ds_read_b32 v203, v8 offset:7680
	s_waitcnt lgkmcnt(0)
	v_max_f32_e32 v170, v170, v170
	v_max_f32_e32 v171, v171, v171
	v_max_f32_e32 v172, v172, v172
	v_max_f32_e32 v173, v173, v173
	v_max_f32_e32 v174, v174, v174
	v_max_f32_e32 v175, v175, v175
	v_max_f32_e32 v176, v176, v176
	v_max_f32_e32 v177, v177, v177
	v_max_f32_e32 v196, v196, v196
	v_max_f32_e32 v197, v197, v197
	v_max_f32_e32 v198, v198, v198
	v_max_f32_e32 v199, v199, v199
	v_max_f32_e32 v200, v200, v200
	v_max_f32_e32 v201, v201, v201
	v_max_f32_e32 v202, v202, v202
	v_max_f32_e32 v203, v203, v203
	v_med3_f32 v170, v170, s20, v13
	v_med3_f32 v171, v171, s20, v13
	v_med3_f32 v172, v172, s20, v13
	v_med3_f32 v173, v173, s20, v13
	v_med3_f32 v174, v174, s20, v13
	v_med3_f32 v175, v175, s20, v13
	v_med3_f32 v176, v176, s20, v13
	v_med3_f32 v177, v177, s20, v13
	v_med3_f32 v196, v196, s20, v13
	v_med3_f32 v197, v197, s20, v13
	v_med3_f32 v198, v198, s20, v13
	v_med3_f32 v199, v199, s20, v13
	v_med3_f32 v200, v200, s20, v13
	v_med3_f32 v201, v201, s20, v13
	v_med3_f32 v202, v202, s20, v13
	v_med3_f32 v203, v203, s20, v13
	v_mov_b32_e32 v208, 0
	v_mov_b32_e32 v209, 0
	v_mov_b32_e32 v210, 0
	v_mov_b32_e32 v211, 0
	v_cvt_pk_fp8_f32 v208, v170, v171
	v_cvt_pk_fp8_f32 v209, v174, v175
	v_cvt_pk_fp8_f32 v210, v196, v197
	v_cvt_pk_fp8_f32 v211, v200, v201
	v_cvt_pk_fp8_f32 v208, v172, v173 op_sel:[0,0,1]
	v_cvt_pk_fp8_f32 v209, v176, v177 op_sel:[0,0,1]
	v_cvt_pk_fp8_f32 v210, v198, v199 op_sel:[0,0,1]
	v_cvt_pk_fp8_f32 v211, v202, v203 op_sel:[0,0,1]
	s_nop 0
	global_store_dwordx4 v12, v[208:211], s[14:15]
	s_waitcnt vmcnt(26)
	v_mul_f32_e32 v68, 0x43000000, v68
	v_mul_f32_e32 v69, 0x43000000, v69
	v_mul_f32_e32 v70, 0x43000000, v70
	v_mul_f32_e32 v71, 0x43000000, v71
	ds_write_b128 v5, v[68:71]
	v_mul_f32_e32 v72, 0x43000000, v72
	v_mul_f32_e32 v73, 0x43000000, v73
	v_mul_f32_e32 v74, 0x43000000, v74
	v_mul_f32_e32 v75, 0x43000000, v75
	ds_write_b128 v5, v[72:75] offset:1024
	v_mul_f32_e32 v76, 0x43000000, v76
	v_mul_f32_e32 v77, 0x43000000, v77
	v_mul_f32_e32 v78, 0x43000000, v78
	v_mul_f32_e32 v79, 0x43000000, v79
	ds_write_b128 v5, v[76:79] offset:2048
	v_mul_f32_e32 v80, 0x43000000, v80
	v_mul_f32_e32 v81, 0x43000000, v81
	v_mul_f32_e32 v82, 0x43000000, v82
	v_mul_f32_e32 v83, 0x43000000, v83
	ds_write_b128 v5, v[80:83] offset:3072
	v_mul_f32_e32 v84, 0x43000000, v84
	v_mul_f32_e32 v85, 0x43000000, v85
	v_mul_f32_e32 v86, 0x43000000, v86
	v_mul_f32_e32 v87, 0x43000000, v87
	ds_write_b128 v5, v[84:87] offset:4096
	v_mul_f32_e32 v88, 0x43000000, v88
	v_mul_f32_e32 v89, 0x43000000, v89
	v_mul_f32_e32 v90, 0x43000000, v90
	v_mul_f32_e32 v91, 0x43000000, v91
	ds_write_b128 v5, v[88:91] offset:5120
	v_mul_f32_e32 v92, 0x43000000, v92
	v_mul_f32_e32 v93, 0x43000000, v93
	v_mul_f32_e32 v94, 0x43000000, v94
	v_mul_f32_e32 v95, 0x43000000, v95
	ds_write_b128 v5, v[92:95] offset:6144
	v_mul_f32_e32 v96, 0x43000000, v96
	v_mul_f32_e32 v97, 0x43000000, v97
	v_mul_f32_e32 v98, 0x43000000, v98
	v_mul_f32_e32 v99, 0x43000000, v99
	ds_write_b128 v5, v[96:99] offset:7168
	s_waitcnt lgkmcnt(0)
	s_barrier
; #define GAS __attribute__((address_space(1)))
; #define LAS __attribute__((address_space(3)))
; #define LDS_WAIT() asm volatile("s_waitcnt lgkmcnt(0)" ::: "memory")
;     const int pr = item >> 1, kb = 2 * (pr / nblk) + (item & 1), nb = pr % nblk, k0 = 64 * kb, n0 = 32 * nb;
;     const int nr = n0 + (lane & 31); const int sc = MAP == 1 ? src_col_in(nr) : nr;
;     float v[32];
; #pragma unroll
;     for (int i = 0; i < 32; ++i) v[i] = sc >= 0 ? W[(size_t)(k0 + 2 * i + (lane >> 5)) * Nsrc + sc] : 0.f;
; #pragma unroll
;     for (int i = 0; i < 32; ++i) { const int k = k0 + 2 * i + (lane >> 5); float x = v[i] * wscale; if (KS) x *= (k < ksplit ? ksA[k] : ksB[k - ksplit]); scr[(2 * i + (lane >> 5)) * 33 + (lane & 31)] = x; }
;     LDS_WAIT(); asm volatile("" ::: "memory");
;     const int c = lane & 7;
; #pragma unroll
;     for (int j = 0; j < 4; ++j) { const int n = (lane >> 3) + 8 * j; const LAS float* s = scr + (8 * c) * 33 + n;
;         const unsigned long long o = (unsigned long long)pg8::pk4_fp8(s[0 * 33], s[1 * 33], s[2 * 33], s[3 * 33]) | ((unsigned long long)pg8::pk4_fp8(s[4 * 33], s[5 * 33], s[6 * 33], s[7 * 33]) << 32);
;         *(GAS unsigned long long*)(WT + (size_t)(n0 + n) * K + k0 + 8 * c) = o; }
;     LDS_WAIT(); asm volatile("" ::: "memory");
; __global__ void __launch_bounds__(NWAVES * 64, 2) hybrid_fwd(Args args) {
;     ...
;             p0_transpose_item_f8<false>(args.in[16] + (size_t)l * FF * DM, FF, DM, DM / 32, (unsigned char*)(ws + WS_WDN + l * SZ_WDN), 128.f, args.in[16], args.in[16], 0, scr, r, lane);
	s_add_i32 s17, s16, 480
	s_min_u32 s17, s17, 0xfff
	s_lshr_b32 s18, s17, 5
	s_add_i32 s18, s18, 0
	s_and_b32 s19, s17, 31
	s_lshl_b32 s18, s18, 21
	s_lshl_b32 s19, s19, 9
	s_add_u32 s18, s18, s19
	s_add_u32 s12, s2, s18
	s_addc_u32 s13, s3, 0
	global_load_dwordx4 v[68:71], v10, s[12:13]
	s_add_u32 s12, s12, 0x8000
	s_addc_u32 s13, s13, 0
	global_load_dwordx4 v[72:75], v10, s[12:13]
	s_add_u32 s12, s12, 0x8000
	s_addc_u32 s13, s13, 0
	global_load_dwordx4 v[76:79], v10, s[12:13]
	s_add_u32 s12, s12, 0x8000
	s_addc_u32 s13, s13, 0
	global_load_dwordx4 v[80:83], v10, s[12:13]
	s_add_u32 s12, s12, 0x8000
	s_addc_u32 s13, s13, 0
	global_load_dwordx4 v[84:87], v10, s[12:13]
	s_add_u32 s12, s12, 0x8000
	s_addc_u32 s13, s13, 0
	global_load_dwordx4 v[88:91], v10, s[12:13]
	s_add_u32 s12, s12, 0x8000
	s_addc_u32 s13, s13, 0
	global_load_dwordx4 v[92:95], v10, s[12:13]
	s_add_u32 s12, s12, 0x8000
	s_addc_u32 s13, s13, 0
	global_load_dwordx4 v[96:99], v10, s[12:13]
	s_add_i32 s17, s16, 96
	s_min_u32 s17, s17, 0xfff
	s_lshr_b32 s18, s17, 5
	s_add_i32 s18, s18, 0
	s_and_b32 s19, s17, 31
	s_lshl_b32 s19, s19, 21
	s_lshl_b32 s18, s18, 7
	s_add_u32 s18, s18, s19
	s_add_u32 s14, s4, s18
	s_addc_u32 s15, s5, 0
	ds_read_b32 v170, v7
	ds_read_b32 v171, v7 offset:512
	ds_read_b32 v172, v7 offset:1024
	ds_read_b32 v173, v7 offset:1536
	ds_read_b32 v174, v7 offset:2048
	ds_read_b32 v175, v7 offset:2560
	ds_read_b32 v176, v7 offset:3072
	ds_read_b32 v177, v7 offset:3584
	ds_read_b32 v196, v7 offset:4096
	ds_read_b32 v197, v7 offset:4608
	ds_read_b32 v198, v7 offset:5120
	ds_read_b32 v199, v7 offset:5632
	ds_read_b32 v200, v7 offset:6144
	ds_read_b32 v201, v7 offset:6656
	ds_read_b32 v202, v7 offset:7168
	ds_read_b32 v203, v7 offset:7680
	s_waitcnt lgkmcnt(0)
	v_max_f32_e32 v170, v170, v170
	v_max_f32_e32 v171, v171, v171
	v_max_f32_e32 v172, v172, v172
	v_max_f32_e32 v173, v173, v173
	v_max_f32_e32 v174, v174, v174
	v_max_f32_e32 v175, v175, v175
	v_max_f32_e32 v176, v176, v176
	v_max_f32_e32 v177, v177, v177
	v_max_f32_e32 v196, v196, v196
	v_max_f32_e32 v197, v197, v197
	v_max_f32_e32 v198, v198, v198
	v_max_f32_e32 v199, v199, v199
	v_max_f32_e32 v200, v200, v200
	v_max_f32_e32 v201, v201, v201
	v_max_f32_e32 v202, v202, v202
	v_max_f32_e32 v203, v203, v203
	v_med3_f32 v170, v170, s20, v13
	v_med3_f32 v171, v171, s20, v13
	v_med3_f32 v172, v172, s20, v13
	v_med3_f32 v173, v173, s20, v13
	v_med3_f32 v174, v174, s20, v13
	v_med3_f32 v175, v175, s20, v13
	v_med3_f32 v176, v176, s20, v13
	v_med3_f32 v177, v177, s20, v13
	v_med3_f32 v196, v196, s20, v13
	v_med3_f32 v197, v197, s20, v13
	v_med3_f32 v198, v198, s20, v13
	v_med3_f32 v199, v199, s20, v13
	v_med3_f32 v200, v200, s20, v13
	v_med3_f32 v201, v201, s20, v13
	v_med3_f32 v202, v202, s20, v13
	v_med3_f32 v203, v203, s20, v13
	v_mov_b32_e32 v208, 0
	v_mov_b32_e32 v209, 0
	v_mov_b32_e32 v210, 0
	v_mov_b32_e32 v211, 0
	v_cvt_pk_fp8_f32 v208, v170, v171
	v_cvt_pk_fp8_f32 v209, v174, v175
	v_cvt_pk_fp8_f32 v210, v196, v197
	v_cvt_pk_fp8_f32 v211, v200, v201
	v_cvt_pk_fp8_f32 v208, v172, v173 op_sel:[0,0,1]
	v_cvt_pk_fp8_f32 v209, v176, v177 op_sel:[0,0,1]
	v_cvt_pk_fp8_f32 v210, v198, v199 op_sel:[0,0,1]
	v_cvt_pk_fp8_f32 v211, v202, v203 op_sel:[0,0,1]
	s_nop 0
	global_store_dwordx4 v11, v[208:211], s[14:15]
	ds_read_b32 v170, v9
	ds_read_b32 v171, v9 offset:512
	ds_read_b32 v172, v9 offset:1024
	ds_read_b32 v173, v9 offset:1536
	ds_read_b32 v174, v9 offset:2048
	ds_read_b32 v175, v9 offset:2560
	ds_read_b32 v176, v9 offset:3072
	ds_read_b32 v177, v9 offset:3584
	ds_read_b32 v196, v9 offset:4096
	ds_read_b32 v197, v9 offset:4608
	ds_read_b32 v198, v9 offset:5120
	ds_read_b32 v199, v9 offset:5632
	ds_read_b32 v200, v9 offset:6144
	ds_read_b32 v201, v9 offset:6656
	ds_read_b32 v202, v9 offset:7168
	ds_read_b32 v203, v9 offset:7680
	s_waitcnt lgkmcnt(0)
	v_max_f32_e32 v170, v170, v170
	v_max_f32_e32 v171, v171, v171
	v_max_f32_e32 v172, v172, v172
	v_max_f32_e32 v173, v173, v173
	v_max_f32_e32 v174, v174, v174
	v_max_f32_e32 v175, v175, v175
	v_max_f32_e32 v176, v176, v176
	v_max_f32_e32 v177, v177, v177
	v_max_f32_e32 v196, v196, v196
	v_max_f32_e32 v197, v197, v197
	v_max_f32_e32 v198, v198, v198
	v_max_f32_e32 v199, v199, v199
	v_max_f32_e32 v200, v200, v200
	v_max_f32_e32 v201, v201, v201
	v_max_f32_e32 v202, v202, v202
	v_max_f32_e32 v203, v203, v203
	v_med3_f32 v170, v170, s20, v13
	v_med3_f32 v171, v171, s20, v13
	v_med3_f32 v172, v172, s20, v13
	v_med3_f32 v173, v173, s20, v13
	v_med3_f32 v174, v174, s20, v13
	v_med3_f32 v175, v175, s20, v13
	v_med3_f32 v176, v176, s20, v13
	v_med3_f32 v177, v177, s20, v13
	v_med3_f32 v196, v196, s20, v13
	v_med3_f32 v197, v197, s20, v13
	v_med3_f32 v198, v198, s20, v13
	v_med3_f32 v199, v199, s20, v13
	v_med3_f32 v200, v200, s20, v13
	v_med3_f32 v201, v201, s20, v13
	v_med3_f32 v202, v202, s20, v13
	v_med3_f32 v203, v203, s20, v13
	v_mov_b32_e32 v208, 0
	v_mov_b32_e32 v209, 0
	v_mov_b32_e32 v210, 0
	v_mov_b32_e32 v211, 0
	v_cvt_pk_fp8_f32 v208, v170, v171
	v_cvt_pk_fp8_f32 v209, v174, v175
	v_cvt_pk_fp8_f32 v210, v196, v197
	v_cvt_pk_fp8_f32 v211, v200, v201
	v_cvt_pk_fp8_f32 v208, v172, v173 op_sel:[0,0,1]
	v_cvt_pk_fp8_f32 v209, v176, v177 op_sel:[0,0,1]
	v_cvt_pk_fp8_f32 v210, v198, v199 op_sel:[0,0,1]
	v_cvt_pk_fp8_f32 v211, v202, v203 op_sel:[0,0,1]
	s_nop 0
	global_store_dwordx4 v12, v[208:211], s[14:15]
	s_waitcnt vmcnt(28)
	v_mul_f32_e32 v100, 0x43000000, v100
	v_mul_f32_e32 v101, 0x43000000, v101
	v_mul_f32_e32 v102, 0x43000000, v102
	v_mul_f32_e32 v103, 0x43000000, v103
	ds_write_b128 v4, v[100:103]
	v_mul_f32_e32 v104, 0x43000000, v104
	v_mul_f32_e32 v105, 0x43000000, v105
	v_mul_f32_e32 v106, 0x43000000, v106
	v_mul_f32_e32 v107, 0x43000000, v107
	ds_write_b128 v4, v[104:107] offset:1024
	v_mul_f32_e32 v108, 0x43000000, v108
	v_mul_f32_e32 v109, 0x43000000, v109
	v_mul_f32_e32 v110, 0x43000000, v110
	v_mul_f32_e32 v111, 0x43000000, v111
	ds_write_b128 v4, v[108:111] offset:2048
	v_mul_f32_e32 v112, 0x43000000, v112
	v_mul_f32_e32 v113, 0x43000000, v113
	v_mul_f32_e32 v114, 0x43000000, v114
	v_mul_f32_e32 v115, 0x43000000, v115
	ds_write_b128 v4, v[112:115] offset:3072
	v_mul_f32_e32 v116, 0x43000000, v116
	v_mul_f32_e32 v117, 0x43000000, v117
	v_mul_f32_e32 v118, 0x43000000, v118
	v_mul_f32_e32 v119, 0x43000000, v119
	ds_write_b128 v4, v[116:119] offset:4096
	v_mul_f32_e32 v120, 0x43000000, v120
	v_mul_f32_e32 v121, 0x43000000, v121
	v_mul_f32_e32 v122, 0x43000000, v122
	v_mul_f32_e32 v123, 0x43000000, v123
	ds_write_b128 v4, v[120:123] offset:5120
	v_mul_f32_e32 v124, 0x43000000, v124
	v_mul_f32_e32 v125, 0x43000000, v125
	v_mul_f32_e32 v126, 0x43000000, v126
	v_mul_f32_e32 v127, 0x43000000, v127
	ds_write_b128 v4, v[124:127] offset:6144
	v_mul_f32_e32 v128, 0x43000000, v128
	v_mul_f32_e32 v129, 0x43000000, v129
	v_mul_f32_e32 v130, 0x43000000, v130
	v_mul_f32_e32 v131, 0x43000000, v131
	ds_write_b128 v4, v[128:131] offset:7168
	s_waitcnt lgkmcnt(0)
	s_barrier
; #define GAS __attribute__((address_space(1)))
; #define LAS __attribute__((address_space(3)))
; #define LDS_WAIT() asm volatile("s_waitcnt lgkmcnt(0)" ::: "memory")
;     const int pr = item >> 1, kb = 2 * (pr / nblk) + (item & 1), nb = pr % nblk, k0 = 64 * kb, n0 = 32 * nb;
;     const int nr = n0 + (lane & 31); const int sc = MAP == 1 ? src_col_in(nr) : nr;
;     float v[32];
; #pragma unroll
;     for (int i = 0; i < 32; ++i) v[i] = sc >= 0 ? W[(size_t)(k0 + 2 * i + (lane >> 5)) * Nsrc + sc] : 0.f;
; #pragma unroll
;     for (int i = 0; i < 32; ++i) { const int k = k0 + 2 * i + (lane >> 5); float x = v[i] * wscale; if (KS) x *= (k < ksplit ? ksA[k] : ksB[k - ksplit]); scr[(2 * i + (lane >> 5)) * 33 + (lane & 31)] = x; }
;     LDS_WAIT(); asm volatile("" ::: "memory");
;     const int c = lane & 7;
; #pragma unroll
;     for (int j = 0; j < 4; ++j) { const int n = (lane >> 3) + 8 * j; const LAS float* s = scr + (8 * c) * 33 + n;
;         const unsigned long long o = (unsigned long long)pg8::pk4_fp8(s[0 * 33], s[1 * 33], s[2 * 33], s[3 * 33]) | ((unsigned long long)pg8::pk4_fp8(s[4 * 33], s[5 * 33], s[6 * 33], s[7 * 33]) << 32);
;         *(GAS unsigned long long*)(WT + (size_t)(n0 + n) * K + k0 + 8 * c) = o; }
;     LDS_WAIT(); asm volatile("" ::: "memory");
; __global__ void __launch_bounds__(NWAVES * 64, 2) hybrid_fwd(Args args) {
;     ...
;             p0_transpose_item_f8<false>(args.in[16] + (size_t)l * FF * DM, FF, DM, DM / 32, (unsigned char*)(ws + WS_WDN + l * SZ_WDN), 128.f, args.in[16], args.in[16], 0, scr, r, lane);
	s_add_i32 s17, s16, 576
	s_min_u32 s17, s17, 0xfff
	s_lshr_b32 s18, s17, 5
	s_add_i32 s18, s18, 0
	s_and_b32 s19, s17, 31
	s_lshl_b32 s18, s18, 21
	s_lshl_b32 s19, s19, 9
	s_add_u32 s18, s18, s19
	s_add_u32 s12, s2, s18
	s_addc_u32 s13, s3, 0
	global_load_dwordx4 v[100:103], v10, s[12:13]
	s_add_u32 s12, s12, 0x8000
	s_addc_u32 s13, s13, 0
	global_load_dwordx4 v[104:107], v10, s[12:13]
	s_add_u32 s12, s12, 0x8000
	s_addc_u32 s13, s13, 0
	global_load_dwordx4 v[108:111], v10, s[12:13]
	s_add_u32 s12, s12, 0x8000
	s_addc_u32 s13, s13, 0
	global_load_dwordx4 v[112:115], v10, s[12:13]
	s_add_u32 s12, s12, 0x8000
	s_addc_u32 s13, s13, 0
	global_load_dwordx4 v[116:119], v10, s[12:13]
	s_add_u32 s12, s12, 0x8000
	s_addc_u32 s13, s13, 0
	global_load_dwordx4 v[120:123], v10, s[12:13]
	s_add_u32 s12, s12, 0x8000
	s_addc_u32 s13, s13, 0
	global_load_dwordx4 v[124:127], v10, s[12:13]
	s_add_u32 s12, s12, 0x8000
	s_addc_u32 s13, s13, 0
	global_load_dwordx4 v[128:131], v10, s[12:13]
	s_add_i32 s17, s16, 192
	s_min_u32 s17, s17, 0xfff
	s_lshr_b32 s18, s17, 5
	s_add_i32 s18, s18, 0
	s_and_b32 s19, s17, 31
	s_lshl_b32 s19, s19, 21
	s_lshl_b32 s18, s18, 7
	s_add_u32 s18, s18, s19
	s_add_u32 s14, s4, s18
	s_addc_u32 s15, s5, 0
	ds_read_b32 v170, v6
	ds_read_b32 v171, v6 offset:512
	ds_read_b32 v172, v6 offset:1024
	ds_read_b32 v173, v6 offset:1536
	ds_read_b32 v174, v6 offset:2048
	ds_read_b32 v175, v6 offset:2560
	ds_read_b32 v176, v6 offset:3072
	ds_read_b32 v177, v6 offset:3584
	ds_read_b32 v196, v6 offset:4096
	ds_read_b32 v197, v6 offset:4608
	ds_read_b32 v198, v6 offset:5120
	ds_read_b32 v199, v6 offset:5632
	ds_read_b32 v200, v6 offset:6144
	ds_read_b32 v201, v6 offset:6656
	ds_read_b32 v202, v6 offset:7168
	ds_read_b32 v203, v6 offset:7680
	s_waitcnt lgkmcnt(0)
	v_max_f32_e32 v170, v170, v170
	v_max_f32_e32 v171, v171, v171
	v_max_f32_e32 v172, v172, v172
	v_max_f32_e32 v173, v173, v173
	v_max_f32_e32 v174, v174, v174
	v_max_f32_e32 v175, v175, v175
	v_max_f32_e32 v176, v176, v176
	v_max_f32_e32 v177, v177, v177
	v_max_f32_e32 v196, v196, v196
	v_max_f32_e32 v197, v197, v197
	v_max_f32_e32 v198, v198, v198
	v_max_f32_e32 v199, v199, v199
	v_max_f32_e32 v200, v200, v200
	v_max_f32_e32 v201, v201, v201
	v_max_f32_e32 v202, v202, v202
	v_max_f32_e32 v203, v203, v203
	v_med3_f32 v170, v170, s20, v13
	v_med3_f32 v171, v171, s20, v13
	v_med3_f32 v172, v172, s20, v13
	v_med3_f32 v173, v173, s20, v13
	v_med3_f32 v174, v174, s20, v13
	v_med3_f32 v175, v175, s20, v13
	v_med3_f32 v176, v176, s20, v13
	v_med3_f32 v177, v177, s20, v13
	v_med3_f32 v196, v196, s20, v13
	v_med3_f32 v197, v197, s20, v13
	v_med3_f32 v198, v198, s20, v13
	v_med3_f32 v199, v199, s20, v13
	v_med3_f32 v200, v200, s20, v13
	v_med3_f32 v201, v201, s20, v13
	v_med3_f32 v202, v202, s20, v13
	v_med3_f32 v203, v203, s20, v13
	v_mov_b32_e32 v208, 0
	v_mov_b32_e32 v209, 0
	v_mov_b32_e32 v210, 0
	v_mov_b32_e32 v211, 0
	v_cvt_pk_fp8_f32 v208, v170, v171
	v_cvt_pk_fp8_f32 v209, v174, v175
	v_cvt_pk_fp8_f32 v210, v196, v197
	v_cvt_pk_fp8_f32 v211, v200, v201
	v_cvt_pk_fp8_f32 v208, v172, v173 op_sel:[0,0,1]
	v_cvt_pk_fp8_f32 v209, v176, v177 op_sel:[0,0,1]
	v_cvt_pk_fp8_f32 v210, v198, v199 op_sel:[0,0,1]
	v_cvt_pk_fp8_f32 v211, v202, v203 op_sel:[0,0,1]
	s_nop 0
	global_store_dwordx4 v11, v[208:211], s[14:15]
	ds_read_b32 v170, v8
	ds_read_b32 v171, v8 offset:512
	ds_read_b32 v172, v8 offset:1024
	ds_read_b32 v173, v8 offset:1536
	ds_read_b32 v174, v8 offset:2048
	ds_read_b32 v175, v8 offset:2560
	ds_read_b32 v176, v8 offset:3072
	ds_read_b32 v177, v8 offset:3584
	ds_read_b32 v196, v8 offset:4096
	ds_read_b32 v197, v8 offset:4608
	ds_read_b32 v198, v8 offset:5120
	ds_read_b32 v199, v8 offset:5632
	ds_read_b32 v200, v8 offset:6144
	ds_read_b32 v201, v8 offset:6656
	ds_read_b32 v202, v8 offset:7168
	ds_read_b32 v203, v8 offset:7680
	s_waitcnt lgkmcnt(0)
	v_max_f32_e32 v170, v170, v170
	v_max_f32_e32 v171, v171, v171
	v_max_f32_e32 v172, v172, v172
	v_max_f32_e32 v173, v173, v173
	v_max_f32_e32 v174, v174, v174
	v_max_f32_e32 v175, v175, v175
	v_max_f32_e32 v176, v176, v176
	v_max_f32_e32 v177, v177, v177
	v_max_f32_e32 v196, v196, v196
	v_max_f32_e32 v197, v197, v197
	v_max_f32_e32 v198, v198, v198
	v_max_f32_e32 v199, v199, v199
	v_max_f32_e32 v200, v200, v200
	v_max_f32_e32 v201, v201, v201
	v_max_f32_e32 v202, v202, v202
	v_max_f32_e32 v203, v203, v203
	v_med3_f32 v170, v170, s20, v13
	v_med3_f32 v171, v171, s20, v13
	v_med3_f32 v172, v172, s20, v13
	v_med3_f32 v173, v173, s20, v13
	v_med3_f32 v174, v174, s20, v13
	v_med3_f32 v175, v175, s20, v13
	v_med3_f32 v176, v176, s20, v13
	v_med3_f32 v177, v177, s20, v13
	v_med3_f32 v196, v196, s20, v13
	v_med3_f32 v197, v197, s20, v13
	v_med3_f32 v198, v198, s20, v13
	v_med3_f32 v199, v199, s20, v13
	v_med3_f32 v200, v200, s20, v13
	v_med3_f32 v201, v201, s20, v13
	v_med3_f32 v202, v202, s20, v13
	v_med3_f32 v203, v203, s20, v13
	v_mov_b32_e32 v208, 0
	v_mov_b32_e32 v209, 0
	v_mov_b32_e32 v210, 0
	v_mov_b32_e32 v211, 0
	v_cvt_pk_fp8_f32 v208, v170, v171
	v_cvt_pk_fp8_f32 v209, v174, v175
	v_cvt_pk_fp8_f32 v210, v196, v197
	v_cvt_pk_fp8_f32 v211, v200, v201
	v_cvt_pk_fp8_f32 v208, v172, v173 op_sel:[0,0,1]
	v_cvt_pk_fp8_f32 v209, v176, v177 op_sel:[0,0,1]
	v_cvt_pk_fp8_f32 v210, v198, v199 op_sel:[0,0,1]
	v_cvt_pk_fp8_f32 v211, v202, v203 op_sel:[0,0,1]
	s_nop 0
	global_store_dwordx4 v12, v[208:211], s[14:15]
	s_waitcnt vmcnt(30)
	v_mul_f32_e32 v132, 0x43000000, v132
	v_mul_f32_e32 v133, 0x43000000, v133
	v_mul_f32_e32 v134, 0x43000000, v134
	v_mul_f32_e32 v135, 0x43000000, v135
	ds_write_b128 v5, v[132:135]
	v_mul_f32_e32 v136, 0x43000000, v136
	v_mul_f32_e32 v137, 0x43000000, v137
	v_mul_f32_e32 v138, 0x43000000, v138
	v_mul_f32_e32 v139, 0x43000000, v139
	ds_write_b128 v5, v[136:139] offset:1024
	v_mul_f32_e32 v140, 0x43000000, v140
	v_mul_f32_e32 v141, 0x43000000, v141
	v_mul_f32_e32 v142, 0x43000000, v142
	v_mul_f32_e32 v143, 0x43000000, v143
	ds_write_b128 v5, v[140:143] offset:2048
	v_mul_f32_e32 v144, 0x43000000, v144
	v_mul_f32_e32 v145, 0x43000000, v145
	v_mul_f32_e32 v146, 0x43000000, v146
	v_mul_f32_e32 v147, 0x43000000, v147
	ds_write_b128 v5, v[144:147] offset:3072
	v_mul_f32_e32 v148, 0x43000000, v148
	v_mul_f32_e32 v149, 0x43000000, v149
	v_mul_f32_e32 v150, 0x43000000, v150
	v_mul_f32_e32 v151, 0x43000000, v151
	ds_write_b128 v5, v[148:151] offset:4096
	v_mul_f32_e32 v152, 0x43000000, v152
	v_mul_f32_e32 v153, 0x43000000, v153
	v_mul_f32_e32 v154, 0x43000000, v154
	v_mul_f32_e32 v155, 0x43000000, v155
	ds_write_b128 v5, v[152:155] offset:5120
	v_mul_f32_e32 v156, 0x43000000, v156
	v_mul_f32_e32 v157, 0x43000000, v157
	v_mul_f32_e32 v158, 0x43000000, v158
	v_mul_f32_e32 v159, 0x43000000, v159
	ds_write_b128 v5, v[156:159] offset:6144
	v_mul_f32_e32 v160, 0x43000000, v160
	v_mul_f32_e32 v161, 0x43000000, v161
	v_mul_f32_e32 v162, 0x43000000, v162
	v_mul_f32_e32 v163, 0x43000000, v163
	ds_write_b128 v5, v[160:163] offset:7168
	s_waitcnt lgkmcnt(0)
	s_barrier
; #define GAS __attribute__((address_space(1)))
; #define LAS __attribute__((address_space(3)))
; #define LDS_WAIT() asm volatile("s_waitcnt lgkmcnt(0)" ::: "memory")
;     const int pr = item >> 1, kb = 2 * (pr / nblk) + (item & 1), nb = pr % nblk, k0 = 64 * kb, n0 = 32 * nb;
;     const int nr = n0 + (lane & 31); const int sc = MAP == 1 ? src_col_in(nr) : nr;
;     float v[32];
; #pragma unroll
;     for (int i = 0; i < 32; ++i) v[i] = sc >= 0 ? W[(size_t)(k0 + 2 * i + (lane >> 5)) * Nsrc + sc] : 0.f;
; #pragma unroll
;     for (int i = 0; i < 32; ++i) { const int k = k0 + 2 * i + (lane >> 5); float x = v[i] * wscale; if (KS) x *= (k < ksplit ? ksA[k] : ksB[k - ksplit]); scr[(2 * i + (lane >> 5)) * 33 + (lane & 31)] = x; }
;     LDS_WAIT(); asm volatile("" ::: "memory");
;     const int c = lane & 7;
; #pragma unroll
;     for (int j = 0; j < 4; ++j) { const int n = (lane >> 3) + 8 * j; const LAS float* s = scr + (8 * c) * 33 + n;
;         const unsigned long long o = (unsigned long long)pg8::pk4_fp8(s[0 * 33], s[1 * 33], s[2 * 33], s[3 * 33]) | ((unsigned long long)pg8::pk4_fp8(s[4 * 33], s[5 * 33], s[6 * 33], s[7 * 33]) << 32);
;         *(GAS unsigned long long*)(WT + (size_t)(n0 + n) * K + k0 + 8 * c) = o; }
;     LDS_WAIT(); asm volatile("" ::: "memory");
; __global__ void __launch_bounds__(NWAVES * 64, 2) hybrid_fwd(Args args) {
;     ...
;             p0_transpose_item_f8<false>(args.in[16] + (size_t)l * FF * DM, FF, DM, DM / 32, (unsigned char*)(ws + WS_WDN + l * SZ_WDN), 128.f, args.in[16], args.in[16], 0, scr, r, lane);
	s_add_i32 s17, s16, 672
	s_min_u32 s17, s17, 0xfff
	s_lshr_b32 s18, s17, 5
	s_add_i32 s18, s18, 0
	s_and_b32 s19, s17, 31
	s_lshl_b32 s18, s18, 21
	s_lshl_b32 s19, s19, 9
	s_add_u32 s18, s18, s19
	s_add_u32 s12, s2, s18
	s_addc_u32 s13, s3, 0
	global_load_dwordx4 v[132:135], v10, s[12:13]
	s_add_u32 s12, s12, 0x8000
	s_addc_u32 s13, s13, 0
	global_load_dwordx4 v[136:139], v10, s[12:13]
	s_add_u32 s12, s12, 0x8000
	s_addc_u32 s13, s13, 0
	global_load_dwordx4 v[140:143], v10, s[12:13]
	s_add_u32 s12, s12, 0x8000
	s_addc_u32 s13, s13, 0
	global_load_dwordx4 v[144:147], v10, s[12:13]
	s_add_u32 s12, s12, 0x8000
	s_addc_u32 s13, s13, 0
	global_load_dwordx4 v[148:151], v10, s[12:13]
	s_add_u32 s12, s12, 0x8000
	s_addc_u32 s13, s13, 0
	global_load_dwordx4 v[152:155], v10, s[12:13]
	s_add_u32 s12, s12, 0x8000
	s_addc_u32 s13, s13, 0
	global_load_dwordx4 v[156:159], v10, s[12:13]
	s_add_u32 s12, s12, 0x8000
	s_addc_u32 s13, s13, 0
	global_load_dwordx4 v[160:163], v10, s[12:13]
	s_add_i32 s17, s16, 288
	s_min_u32 s17, s17, 0xfff
	s_lshr_b32 s18, s17, 5
	s_add_i32 s18, s18, 0
	s_and_b32 s19, s17, 31
	s_lshl_b32 s19, s19, 21
	s_lshl_b32 s18, s18, 7
	s_add_u32 s18, s18, s19
	s_add_u32 s14, s4, s18
	s_addc_u32 s15, s5, 0
	ds_read_b32 v170, v7
	ds_read_b32 v171, v7 offset:512
	ds_read_b32 v172, v7 offset:1024
	ds_read_b32 v173, v7 offset:1536
	ds_read_b32 v174, v7 offset:2048
	ds_read_b32 v175, v7 offset:2560
	ds_read_b32 v176, v7 offset:3072
	ds_read_b32 v177, v7 offset:3584
	ds_read_b32 v196, v7 offset:4096
	ds_read_b32 v197, v7 offset:4608
	ds_read_b32 v198, v7 offset:5120
	ds_read_b32 v199, v7 offset:5632
	ds_read_b32 v200, v7 offset:6144
	ds_read_b32 v201, v7 offset:6656
	ds_read_b32 v202, v7 offset:7168
	ds_read_b32 v203, v7 offset:7680
	s_waitcnt lgkmcnt(0)
	v_max_f32_e32 v170, v170, v170
	v_max_f32_e32 v171, v171, v171
	v_max_f32_e32 v172, v172, v172
	v_max_f32_e32 v173, v173, v173
	v_max_f32_e32 v174, v174, v174
	v_max_f32_e32 v175, v175, v175
	v_max_f32_e32 v176, v176, v176
	v_max_f32_e32 v177, v177, v177
	v_max_f32_e32 v196, v196, v196
	v_max_f32_e32 v197, v197, v197
	v_max_f32_e32 v198, v198, v198
	v_max_f32_e32 v199, v199, v199
	v_max_f32_e32 v200, v200, v200
	v_max_f32_e32 v201, v201, v201
	v_max_f32_e32 v202, v202, v202
	v_max_f32_e32 v203, v203, v203
	v_med3_f32 v170, v170, s20, v13
	v_med3_f32 v171, v171, s20, v13
	v_med3_f32 v172, v172, s20, v13
	v_med3_f32 v173, v173, s20, v13
	v_med3_f32 v174, v174, s20, v13
	v_med3_f32 v175, v175, s20, v13
	v_med3_f32 v176, v176, s20, v13
	v_med3_f32 v177, v177, s20, v13
	v_med3_f32 v196, v196, s20, v13
	v_med3_f32 v197, v197, s20, v13
	v_med3_f32 v198, v198, s20, v13
	v_med3_f32 v199, v199, s20, v13
	v_med3_f32 v200, v200, s20, v13
	v_med3_f32 v201, v201, s20, v13
	v_med3_f32 v202, v202, s20, v13
	v_med3_f32 v203, v203, s20, v13
	v_mov_b32_e32 v208, 0
	v_mov_b32_e32 v209, 0
	v_mov_b32_e32 v210, 0
	v_mov_b32_e32 v211, 0
	v_cvt_pk_fp8_f32 v208, v170, v171
	v_cvt_pk_fp8_f32 v209, v174, v175
	v_cvt_pk_fp8_f32 v210, v196, v197
	v_cvt_pk_fp8_f32 v211, v200, v201
	v_cvt_pk_fp8_f32 v208, v172, v173 op_sel:[0,0,1]
	v_cvt_pk_fp8_f32 v209, v176, v177 op_sel:[0,0,1]
	v_cvt_pk_fp8_f32 v210, v198, v199 op_sel:[0,0,1]
	v_cvt_pk_fp8_f32 v211, v202, v203 op_sel:[0,0,1]
	s_nop 0
	global_store_dwordx4 v11, v[208:211], s[14:15]
	ds_read_b32 v170, v9
	ds_read_b32 v171, v9 offset:512
	ds_read_b32 v172, v9 offset:1024
	ds_read_b32 v173, v9 offset:1536
	ds_read_b32 v174, v9 offset:2048
	ds_read_b32 v175, v9 offset:2560
	ds_read_b32 v176, v9 offset:3072
	ds_read_b32 v177, v9 offset:3584
	ds_read_b32 v196, v9 offset:4096
	ds_read_b32 v197, v9 offset:4608
	ds_read_b32 v198, v9 offset:5120
	ds_read_b32 v199, v9 offset:5632
	ds_read_b32 v200, v9 offset:6144
	ds_read_b32 v201, v9 offset:6656
	ds_read_b32 v202, v9 offset:7168
	ds_read_b32 v203, v9 offset:7680
	s_waitcnt lgkmcnt(0)
	v_max_f32_e32 v170, v170, v170
	v_max_f32_e32 v171, v171, v171
	v_max_f32_e32 v172, v172, v172
	v_max_f32_e32 v173, v173, v173
	v_max_f32_e32 v174, v174, v174
	v_max_f32_e32 v175, v175, v175
	v_max_f32_e32 v176, v176, v176
	v_max_f32_e32 v177, v177, v177
	v_max_f32_e32 v196, v196, v196
	v_max_f32_e32 v197, v197, v197
	v_max_f32_e32 v198, v198, v198
	v_max_f32_e32 v199, v199, v199
	v_max_f32_e32 v200, v200, v200
	v_max_f32_e32 v201, v201, v201
	v_max_f32_e32 v202, v202, v202
	v_max_f32_e32 v203, v203, v203
	v_med3_f32 v170, v170, s20, v13
	v_med3_f32 v171, v171, s20, v13
	v_med3_f32 v172, v172, s20, v13
	v_med3_f32 v173, v173, s20, v13
	v_med3_f32 v174, v174, s20, v13
	v_med3_f32 v175, v175, s20, v13
	v_med3_f32 v176, v176, s20, v13
	v_med3_f32 v177, v177, s20, v13
	v_med3_f32 v196, v196, s20, v13
	v_med3_f32 v197, v197, s20, v13
	v_med3_f32 v198, v198, s20, v13
	v_med3_f32 v199, v199, s20, v13
	v_med3_f32 v200, v200, s20, v13
	v_med3_f32 v201, v201, s20, v13
	v_med3_f32 v202, v202, s20, v13
	v_med3_f32 v203, v203, s20, v13
	v_mov_b32_e32 v208, 0
	v_mov_b32_e32 v209, 0
	v_mov_b32_e32 v210, 0
	v_mov_b32_e32 v211, 0
	v_cvt_pk_fp8_f32 v208, v170, v171
	v_cvt_pk_fp8_f32 v209, v174, v175
	v_cvt_pk_fp8_f32 v210, v196, v197
	v_cvt_pk_fp8_f32 v211, v200, v201
	v_cvt_pk_fp8_f32 v208, v172, v173 op_sel:[0,0,1]
	v_cvt_pk_fp8_f32 v209, v176, v177 op_sel:[0,0,1]
	v_cvt_pk_fp8_f32 v210, v198, v199 op_sel:[0,0,1]
	v_cvt_pk_fp8_f32 v211, v202, v203 op_sel:[0,0,1]
	s_nop 0
	global_store_dwordx4 v12, v[208:211], s[14:15]
	s_waitcnt vmcnt(32)
	v_mul_f32_e32 v36, 0x43000000, v36
	v_mul_f32_e32 v37, 0x43000000, v37
	v_mul_f32_e32 v38, 0x43000000, v38
	v_mul_f32_e32 v39, 0x43000000, v39
	ds_write_b128 v4, v[36:39]
	v_mul_f32_e32 v40, 0x43000000, v40
	v_mul_f32_e32 v41, 0x43000000, v41
	v_mul_f32_e32 v42, 0x43000000, v42
	v_mul_f32_e32 v43, 0x43000000, v43
	ds_write_b128 v4, v[40:43] offset:1024
	v_mul_f32_e32 v44, 0x43000000, v44
	v_mul_f32_e32 v45, 0x43000000, v45
	v_mul_f32_e32 v46, 0x43000000, v46
	v_mul_f32_e32 v47, 0x43000000, v47
	ds_write_b128 v4, v[44:47] offset:2048
	v_mul_f32_e32 v48, 0x43000000, v48
	v_mul_f32_e32 v49, 0x43000000, v49
	v_mul_f32_e32 v50, 0x43000000, v50
	v_mul_f32_e32 v51, 0x43000000, v51
	ds_write_b128 v4, v[48:51] offset:3072
	v_mul_f32_e32 v52, 0x43000000, v52
	v_mul_f32_e32 v53, 0x43000000, v53
	v_mul_f32_e32 v54, 0x43000000, v54
	v_mul_f32_e32 v55, 0x43000000, v55
	ds_write_b128 v4, v[52:55] offset:4096
	v_mul_f32_e32 v56, 0x43000000, v56
	v_mul_f32_e32 v57, 0x43000000, v57
	v_mul_f32_e32 v58, 0x43000000, v58
	v_mul_f32_e32 v59, 0x43000000, v59
	ds_write_b128 v4, v[56:59] offset:5120
	v_mul_f32_e32 v60, 0x43000000, v60
	v_mul_f32_e32 v61, 0x43000000, v61
	v_mul_f32_e32 v62, 0x43000000, v62
	v_mul_f32_e32 v63, 0x43000000, v63
	ds_write_b128 v4, v[60:63] offset:6144
	v_mul_f32_e32 v64, 0x43000000, v64
	v_mul_f32_e32 v65, 0x43000000, v65
	v_mul_f32_e32 v66, 0x43000000, v66
	v_mul_f32_e32 v67, 0x43000000, v67
	ds_write_b128 v4, v[64:67] offset:7168
	s_waitcnt lgkmcnt(0)
	s_barrier
; #define GAS __attribute__((address_space(1)))
; #define LAS __attribute__((address_space(3)))
; #define LDS_WAIT() asm volatile("s_waitcnt lgkmcnt(0)" ::: "memory")
;     const int pr = item >> 1, kb = 2 * (pr / nblk) + (item & 1), nb = pr % nblk, k0 = 64 * kb, n0 = 32 * nb;
;     const int nr = n0 + (lane & 31); const int sc = MAP == 1 ? src_col_in(nr) : nr;
;     float v[32];
; #pragma unroll
;     for (int i = 0; i < 32; ++i) v[i] = sc >= 0 ? W[(size_t)(k0 + 2 * i + (lane >> 5)) * Nsrc + sc] : 0.f;
; #pragma unroll
;     for (int i = 0; i < 32; ++i) { const int k = k0 + 2 * i + (lane >> 5); float x = v[i] * wscale; if (KS) x *= (k < ksplit ? ksA[k] : ksB[k - ksplit]); scr[(2 * i + (lane >> 5)) * 33 + (lane & 31)] = x; }
;     LDS_WAIT(); asm volatile("" ::: "memory");
;     const int c = lane & 7;
; #pragma unroll
;     for (int j = 0; j < 4; ++j) { const int n = (lane >> 3) + 8 * j; const LAS float* s = scr + (8 * c) * 33 + n;
;         const unsigned long long o = (unsigned long long)pg8::pk4_fp8(s[0 * 33], s[1 * 33], s[2 * 33], s[3 * 33]) | ((unsigned long long)pg8::pk4_fp8(s[4 * 33], s[5 * 33], s[6 * 33], s[7 * 33]) << 32);
;         *(GAS unsigned long long*)(WT + (size_t)(n0 + n) * K + k0 + 8 * c) = o; }
;     LDS_WAIT(); asm volatile("" ::: "memory");
; __global__ void __launch_bounds__(NWAVES * 64, 2) hybrid_fwd(Args args) {
;     ...
;             p0_transpose_item_f8<false>(args.in[16] + (size_t)l * FF * DM, FF, DM, DM / 32, (unsigned char*)(ws + WS_WDN + l * SZ_WDN), 128.f, args.in[16], args.in[16], 0, scr, r, lane);
	s_add_i32 s17, s16, 768
	s_min_u32 s17, s17, 0xfff
	s_lshr_b32 s18, s17, 5
	s_add_i32 s18, s18, 0
	s_and_b32 s19, s17, 31
	s_lshl_b32 s18, s18, 21
	s_lshl_b32 s19, s19, 9
	s_add_u32 s18, s18, s19
	s_add_u32 s12, s2, s18
	s_addc_u32 s13, s3, 0
	global_load_dwordx4 v[36:39], v10, s[12:13]
	s_add_u32 s12, s12, 0x8000
	s_addc_u32 s13, s13, 0
	global_load_dwordx4 v[40:43], v10, s[12:13]
	s_add_u32 s12, s12, 0x8000
	s_addc_u32 s13, s13, 0
	global_load_dwordx4 v[44:47], v10, s[12:13]
	s_add_u32 s12, s12, 0x8000
	s_addc_u32 s13, s13, 0
	global_load_dwordx4 v[48:51], v10, s[12:13]
	s_add_u32 s12, s12, 0x8000
	s_addc_u32 s13, s13, 0
	global_load_dwordx4 v[52:55], v10, s[12:13]
	s_add_u32 s12, s12, 0x8000
	s_addc_u32 s13, s13, 0
	global_load_dwordx4 v[56:59], v10, s[12:13]
	s_add_u32 s12, s12, 0x8000
	s_addc_u32 s13, s13, 0
	global_load_dwordx4 v[60:63], v10, s[12:13]
	s_add_u32 s12, s12, 0x8000
	s_addc_u32 s13, s13, 0
	global_load_dwordx4 v[64:67], v10, s[12:13]
	s_add_i32 s17, s16, 384
	s_min_u32 s17, s17, 0xfff
	s_lshr_b32 s18, s17, 5
	s_add_i32 s18, s18, 0
	s_and_b32 s19, s17, 31
	s_lshl_b32 s19, s19, 21
	s_lshl_b32 s18, s18, 7
	s_add_u32 s18, s18, s19
	s_add_u32 s14, s4, s18
	s_addc_u32 s15, s5, 0
	ds_read_b32 v170, v6
	ds_read_b32 v171, v6 offset:512
	ds_read_b32 v172, v6 offset:1024
	ds_read_b32 v173, v6 offset:1536
	ds_read_b32 v174, v6 offset:2048
	ds_read_b32 v175, v6 offset:2560
	ds_read_b32 v176, v6 offset:3072
	ds_read_b32 v177, v6 offset:3584
	ds_read_b32 v196, v6 offset:4096
	ds_read_b32 v197, v6 offset:4608
	ds_read_b32 v198, v6 offset:5120
	ds_read_b32 v199, v6 offset:5632
	ds_read_b32 v200, v6 offset:6144
	ds_read_b32 v201, v6 offset:6656
	ds_read_b32 v202, v6 offset:7168
	ds_read_b32 v203, v6 offset:7680
	s_waitcnt lgkmcnt(0)
	v_max_f32_e32 v170, v170, v170
	v_max_f32_e32 v171, v171, v171
	v_max_f32_e32 v172, v172, v172
	v_max_f32_e32 v173, v173, v173
	v_max_f32_e32 v174, v174, v174
	v_max_f32_e32 v175, v175, v175
	v_max_f32_e32 v176, v176, v176
	v_max_f32_e32 v177, v177, v177
	v_max_f32_e32 v196, v196, v196
	v_max_f32_e32 v197, v197, v197
	v_max_f32_e32 v198, v198, v198
	v_max_f32_e32 v199, v199, v199
	v_max_f32_e32 v200, v200, v200
	v_max_f32_e32 v201, v201, v201
	v_max_f32_e32 v202, v202, v202
	v_max_f32_e32 v203, v203, v203
	v_med3_f32 v170, v170, s20, v13
	v_med3_f32 v171, v171, s20, v13
	v_med3_f32 v172, v172, s20, v13
	v_med3_f32 v173, v173, s20, v13
	v_med3_f32 v174, v174, s20, v13
	v_med3_f32 v175, v175, s20, v13
	v_med3_f32 v176, v176, s20, v13
	v_med3_f32 v177, v177, s20, v13
	v_med3_f32 v196, v196, s20, v13
	v_med3_f32 v197, v197, s20, v13
	v_med3_f32 v198, v198, s20, v13
	v_med3_f32 v199, v199, s20, v13
	v_med3_f32 v200, v200, s20, v13
	v_med3_f32 v201, v201, s20, v13
	v_med3_f32 v202, v202, s20, v13
	v_med3_f32 v203, v203, s20, v13
	v_mov_b32_e32 v208, 0
	v_mov_b32_e32 v209, 0
	v_mov_b32_e32 v210, 0
	v_mov_b32_e32 v211, 0
	v_cvt_pk_fp8_f32 v208, v170, v171
	v_cvt_pk_fp8_f32 v209, v174, v175
	v_cvt_pk_fp8_f32 v210, v196, v197
	v_cvt_pk_fp8_f32 v211, v200, v201
	v_cvt_pk_fp8_f32 v208, v172, v173 op_sel:[0,0,1]
	v_cvt_pk_fp8_f32 v209, v176, v177 op_sel:[0,0,1]
	v_cvt_pk_fp8_f32 v210, v198, v199 op_sel:[0,0,1]
	v_cvt_pk_fp8_f32 v211, v202, v203 op_sel:[0,0,1]
	s_nop 0
	global_store_dwordx4 v11, v[208:211], s[14:15]
	ds_read_b32 v170, v8
	ds_read_b32 v171, v8 offset:512
	ds_read_b32 v172, v8 offset:1024
	ds_read_b32 v173, v8 offset:1536
	ds_read_b32 v174, v8 offset:2048
	ds_read_b32 v175, v8 offset:2560
	ds_read_b32 v176, v8 offset:3072
	ds_read_b32 v177, v8 offset:3584
	ds_read_b32 v196, v8 offset:4096
	ds_read_b32 v197, v8 offset:4608
	ds_read_b32 v198, v8 offset:5120
	ds_read_b32 v199, v8 offset:5632
	ds_read_b32 v200, v8 offset:6144
	ds_read_b32 v201, v8 offset:6656
	ds_read_b32 v202, v8 offset:7168
	ds_read_b32 v203, v8 offset:7680
	s_waitcnt lgkmcnt(0)
	v_max_f32_e32 v170, v170, v170
	v_max_f32_e32 v171, v171, v171
	v_max_f32_e32 v172, v172, v172
	v_max_f32_e32 v173, v173, v173
	v_max_f32_e32 v174, v174, v174
	v_max_f32_e32 v175, v175, v175
	v_max_f32_e32 v176, v176, v176
	v_max_f32_e32 v177, v177, v177
	v_max_f32_e32 v196, v196, v196
	v_max_f32_e32 v197, v197, v197
	v_max_f32_e32 v198, v198, v198
	v_max_f32_e32 v199, v199, v199
	v_max_f32_e32 v200, v200, v200
	v_max_f32_e32 v201, v201, v201
	v_max_f32_e32 v202, v202, v202
	v_max_f32_e32 v203, v203, v203
	v_med3_f32 v170, v170, s20, v13
	v_med3_f32 v171, v171, s20, v13
	v_med3_f32 v172, v172, s20, v13
	v_med3_f32 v173, v173, s20, v13
	v_med3_f32 v174, v174, s20, v13
	v_med3_f32 v175, v175, s20, v13
	v_med3_f32 v176, v176, s20, v13
	v_med3_f32 v177, v177, s20, v13
	v_med3_f32 v196, v196, s20, v13
	v_med3_f32 v197, v197, s20, v13
	v_med3_f32 v198, v198, s20, v13
	v_med3_f32 v199, v199, s20, v13
	v_med3_f32 v200, v200, s20, v13
	v_med3_f32 v201, v201, s20, v13
	v_med3_f32 v202, v202, s20, v13
	v_med3_f32 v203, v203, s20, v13
	v_mov_b32_e32 v208, 0
	v_mov_b32_e32 v209, 0
	v_mov_b32_e32 v210, 0
	v_mov_b32_e32 v211, 0
	v_cvt_pk_fp8_f32 v208, v170, v171
	v_cvt_pk_fp8_f32 v209, v174, v175
	v_cvt_pk_fp8_f32 v210, v196, v197
	v_cvt_pk_fp8_f32 v211, v200, v201
	v_cvt_pk_fp8_f32 v208, v172, v173 op_sel:[0,0,1]
	v_cvt_pk_fp8_f32 v209, v176, v177 op_sel:[0,0,1]
	v_cvt_pk_fp8_f32 v210, v198, v199 op_sel:[0,0,1]
	v_cvt_pk_fp8_f32 v211, v202, v203 op_sel:[0,0,1]
	s_nop 0
	global_store_dwordx4 v12, v[208:211], s[14:15]
	s_waitcnt vmcnt(32)
	v_mul_f32_e32 v68, 0x43000000, v68
	v_mul_f32_e32 v69, 0x43000000, v69
	v_mul_f32_e32 v70, 0x43000000, v70
	v_mul_f32_e32 v71, 0x43000000, v71
	ds_write_b128 v5, v[68:71]
	v_mul_f32_e32 v72, 0x43000000, v72
	v_mul_f32_e32 v73, 0x43000000, v73
	v_mul_f32_e32 v74, 0x43000000, v74
	v_mul_f32_e32 v75, 0x43000000, v75
	ds_write_b128 v5, v[72:75] offset:1024
	v_mul_f32_e32 v76, 0x43000000, v76
	v_mul_f32_e32 v77, 0x43000000, v77
	v_mul_f32_e32 v78, 0x43000000, v78
	v_mul_f32_e32 v79, 0x43000000, v79
	ds_write_b128 v5, v[76:79] offset:2048
	v_mul_f32_e32 v80, 0x43000000, v80
	v_mul_f32_e32 v81, 0x43000000, v81
	v_mul_f32_e32 v82, 0x43000000, v82
	v_mul_f32_e32 v83, 0x43000000, v83
	ds_write_b128 v5, v[80:83] offset:3072
	v_mul_f32_e32 v84, 0x43000000, v84
	v_mul_f32_e32 v85, 0x43000000, v85
	v_mul_f32_e32 v86, 0x43000000, v86
	v_mul_f32_e32 v87, 0x43000000, v87
	ds_write_b128 v5, v[84:87] offset:4096
	v_mul_f32_e32 v88, 0x43000000, v88
	v_mul_f32_e32 v89, 0x43000000, v89
	v_mul_f32_e32 v90, 0x43000000, v90
	v_mul_f32_e32 v91, 0x43000000, v91
	ds_write_b128 v5, v[88:91] offset:5120
	v_mul_f32_e32 v92, 0x43000000, v92
	v_mul_f32_e32 v93, 0x43000000, v93
	v_mul_f32_e32 v94, 0x43000000, v94
	v_mul_f32_e32 v95, 0x43000000, v95
	ds_write_b128 v5, v[92:95] offset:6144
	v_mul_f32_e32 v96, 0x43000000, v96
	v_mul_f32_e32 v97, 0x43000000, v97
	v_mul_f32_e32 v98, 0x43000000, v98
	v_mul_f32_e32 v99, 0x43000000, v99
	ds_write_b128 v5, v[96:99] offset:7168
	s_waitcnt lgkmcnt(0)
	s_barrier
; #define GAS __attribute__((address_space(1)))
; #define LAS __attribute__((address_space(3)))
; #define LDS_WAIT() asm volatile("s_waitcnt lgkmcnt(0)" ::: "memory")
;     const int pr = item >> 1, kb = 2 * (pr / nblk) + (item & 1), nb = pr % nblk, k0 = 64 * kb, n0 = 32 * nb;
;     const int nr = n0 + (lane & 31); const int sc = MAP == 1 ? src_col_in(nr) : nr;
;     float v[32];
; #pragma unroll
;     for (int i = 0; i < 32; ++i) v[i] = sc >= 0 ? W[(size_t)(k0 + 2 * i + (lane >> 5)) * Nsrc + sc] : 0.f;
; #pragma unroll
;     for (int i = 0; i < 32; ++i) { const int k = k0 + 2 * i + (lane >> 5); float x = v[i] * wscale; if (KS) x *= (k < ksplit ? ksA[k] : ksB[k - ksplit]); scr[(2 * i + (lane >> 5)) * 33 + (lane & 31)] = x; }
;     LDS_WAIT(); asm volatile("" ::: "memory");
;     const int c = lane & 7;
; #pragma unroll
;     for (int j = 0; j < 4; ++j) { const int n = (lane >> 3) + 8 * j; const LAS float* s = scr + (8 * c) * 33 + n;
;         const unsigned long long o = (unsigned long long)pg8::pk4_fp8(s[0 * 33], s[1 * 33], s[2 * 33], s[3 * 33]) | ((unsigned long long)pg8::pk4_fp8(s[4 * 33], s[5 * 33], s[6 * 33], s[7 * 33]) << 32);
;         *(GAS unsigned long long*)(WT + (size_t)(n0 + n) * K + k0 + 8 * c) = o; }
;     LDS_WAIT(); asm volatile("" ::: "memory");
; __global__ void __launch_bounds__(NWAVES * 64, 2) hybrid_fwd(Args args) {
;     ...
;             p0_transpose_item_f8<false>(args.in[16] + (size_t)l * FF * DM, FF, DM, DM / 32, (unsigned char*)(ws + WS_WDN + l * SZ_WDN), 128.f, args.in[16], args.in[16], 0, scr, r, lane);
	s_add_i32 s17, s16, 864
	s_min_u32 s17, s17, 0xfff
	s_lshr_b32 s18, s17, 5
	s_add_i32 s18, s18, 0
	s_and_b32 s19, s17, 31
	s_lshl_b32 s18, s18, 21
	s_lshl_b32 s19, s19, 9
	s_add_u32 s18, s18, s19
	s_add_u32 s12, s2, s18
	s_addc_u32 s13, s3, 0
	global_load_dwordx4 v[68:71], v10, s[12:13]
	s_add_u32 s12, s12, 0x8000
	s_addc_u32 s13, s13, 0
	global_load_dwordx4 v[72:75], v10, s[12:13]
	s_add_u32 s12, s12, 0x8000
	s_addc_u32 s13, s13, 0
	global_load_dwordx4 v[76:79], v10, s[12:13]
	s_add_u32 s12, s12, 0x8000
	s_addc_u32 s13, s13, 0
	global_load_dwordx4 v[80:83], v10, s[12:13]
	s_add_u32 s12, s12, 0x8000
	s_addc_u32 s13, s13, 0
	global_load_dwordx4 v[84:87], v10, s[12:13]
	s_add_u32 s12, s12, 0x8000
	s_addc_u32 s13, s13, 0
	global_load_dwordx4 v[88:91], v10, s[12:13]
	s_add_u32 s12, s12, 0x8000
	s_addc_u32 s13, s13, 0
	global_load_dwordx4 v[92:95], v10, s[12:13]
	s_add_u32 s12, s12, 0x8000
	s_addc_u32 s13, s13, 0
	global_load_dwordx4 v[96:99], v10, s[12:13]
	s_add_i32 s17, s16, 480
	s_min_u32 s17, s17, 0xfff
	s_lshr_b32 s18, s17, 5
	s_add_i32 s18, s18, 0
	s_and_b32 s19, s17, 31
	s_lshl_b32 s19, s19, 21
	s_lshl_b32 s18, s18, 7
	s_add_u32 s18, s18, s19
	s_add_u32 s14, s4, s18
	s_addc_u32 s15, s5, 0
	ds_read_b32 v170, v7
	ds_read_b32 v171, v7 offset:512
	ds_read_b32 v172, v7 offset:1024
	ds_read_b32 v173, v7 offset:1536
	ds_read_b32 v174, v7 offset:2048
	ds_read_b32 v175, v7 offset:2560
	ds_read_b32 v176, v7 offset:3072
	ds_read_b32 v177, v7 offset:3584
	ds_read_b32 v196, v7 offset:4096
	ds_read_b32 v197, v7 offset:4608
	ds_read_b32 v198, v7 offset:5120
	ds_read_b32 v199, v7 offset:5632
	ds_read_b32 v200, v7 offset:6144
	ds_read_b32 v201, v7 offset:6656
	ds_read_b32 v202, v7 offset:7168
	ds_read_b32 v203, v7 offset:7680
	s_waitcnt lgkmcnt(0)
	v_max_f32_e32 v170, v170, v170
	v_max_f32_e32 v171, v171, v171
	v_max_f32_e32 v172, v172, v172
	v_max_f32_e32 v173, v173, v173
	v_max_f32_e32 v174, v174, v174
	v_max_f32_e32 v175, v175, v175
	v_max_f32_e32 v176, v176, v176
	v_max_f32_e32 v177, v177, v177
	v_max_f32_e32 v196, v196, v196
	v_max_f32_e32 v197, v197, v197
	v_max_f32_e32 v198, v198, v198
	v_max_f32_e32 v199, v199, v199
	v_max_f32_e32 v200, v200, v200
	v_max_f32_e32 v201, v201, v201
	v_max_f32_e32 v202, v202, v202
	v_max_f32_e32 v203, v203, v203
	v_med3_f32 v170, v170, s20, v13
	v_med3_f32 v171, v171, s20, v13
	v_med3_f32 v172, v172, s20, v13
	v_med3_f32 v173, v173, s20, v13
	v_med3_f32 v174, v174, s20, v13
	v_med3_f32 v175, v175, s20, v13
	v_med3_f32 v176, v176, s20, v13
	v_med3_f32 v177, v177, s20, v13
	v_med3_f32 v196, v196, s20, v13
	v_med3_f32 v197, v197, s20, v13
	v_med3_f32 v198, v198, s20, v13
	v_med3_f32 v199, v199, s20, v13
	v_med3_f32 v200, v200, s20, v13
	v_med3_f32 v201, v201, s20, v13
	v_med3_f32 v202, v202, s20, v13
	v_med3_f32 v203, v203, s20, v13
	v_mov_b32_e32 v208, 0
	v_mov_b32_e32 v209, 0
	v_mov_b32_e32 v210, 0
	v_mov_b32_e32 v211, 0
	v_cvt_pk_fp8_f32 v208, v170, v171
	v_cvt_pk_fp8_f32 v209, v174, v175
	v_cvt_pk_fp8_f32 v210, v196, v197
	v_cvt_pk_fp8_f32 v211, v200, v201
	v_cvt_pk_fp8_f32 v208, v172, v173 op_sel:[0,0,1]
	v_cvt_pk_fp8_f32 v209, v176, v177 op_sel:[0,0,1]
	v_cvt_pk_fp8_f32 v210, v198, v199 op_sel:[0,0,1]
	v_cvt_pk_fp8_f32 v211, v202, v203 op_sel:[0,0,1]
	s_nop 0
	global_store_dwordx4 v11, v[208:211], s[14:15]
	ds_read_b32 v170, v9
	ds_read_b32 v171, v9 offset:512
	ds_read_b32 v172, v9 offset:1024
	ds_read_b32 v173, v9 offset:1536
	ds_read_b32 v174, v9 offset:2048
	ds_read_b32 v175, v9 offset:2560
	ds_read_b32 v176, v9 offset:3072
	ds_read_b32 v177, v9 offset:3584
	ds_read_b32 v196, v9 offset:4096
	ds_read_b32 v197, v9 offset:4608
	ds_read_b32 v198, v9 offset:5120
	ds_read_b32 v199, v9 offset:5632
	ds_read_b32 v200, v9 offset:6144
	ds_read_b32 v201, v9 offset:6656
	ds_read_b32 v202, v9 offset:7168
	ds_read_b32 v203, v9 offset:7680
	s_waitcnt lgkmcnt(0)
	v_max_f32_e32 v170, v170, v170
	v_max_f32_e32 v171, v171, v171
	v_max_f32_e32 v172, v172, v172
	v_max_f32_e32 v173, v173, v173
	v_max_f32_e32 v174, v174, v174
	v_max_f32_e32 v175, v175, v175
	v_max_f32_e32 v176, v176, v176
	v_max_f32_e32 v177, v177, v177
	v_max_f32_e32 v196, v196, v196
	v_max_f32_e32 v197, v197, v197
	v_max_f32_e32 v198, v198, v198
	v_max_f32_e32 v199, v199, v199
	v_max_f32_e32 v200, v200, v200
	v_max_f32_e32 v201, v201, v201
	v_max_f32_e32 v202, v202, v202
	v_max_f32_e32 v203, v203, v203
	v_med3_f32 v170, v170, s20, v13
	v_med3_f32 v171, v171, s20, v13
	v_med3_f32 v172, v172, s20, v13
	v_med3_f32 v173, v173, s20, v13
	v_med3_f32 v174, v174, s20, v13
	v_med3_f32 v175, v175, s20, v13
	v_med3_f32 v176, v176, s20, v13
	v_med3_f32 v177, v177, s20, v13
	v_med3_f32 v196, v196, s20, v13
	v_med3_f32 v197, v197, s20, v13
	v_med3_f32 v198, v198, s20, v13
	v_med3_f32 v199, v199, s20, v13
	v_med3_f32 v200, v200, s20, v13
	v_med3_f32 v201, v201, s20, v13
	v_med3_f32 v202, v202, s20, v13
	v_med3_f32 v203, v203, s20, v13
	v_mov_b32_e32 v208, 0
	v_mov_b32_e32 v209, 0
	v_mov_b32_e32 v210, 0
	v_mov_b32_e32 v211, 0
	v_cvt_pk_fp8_f32 v208, v170, v171
	v_cvt_pk_fp8_f32 v209, v174, v175
	v_cvt_pk_fp8_f32 v210, v196, v197
	v_cvt_pk_fp8_f32 v211, v200, v201
	v_cvt_pk_fp8_f32 v208, v172, v173 op_sel:[0,0,1]
	v_cvt_pk_fp8_f32 v209, v176, v177 op_sel:[0,0,1]
	v_cvt_pk_fp8_f32 v210, v198, v199 op_sel:[0,0,1]
	v_cvt_pk_fp8_f32 v211, v202, v203 op_sel:[0,0,1]
	s_nop 0
	global_store_dwordx4 v12, v[208:211], s[14:15]
	s_waitcnt vmcnt(32)
	v_mul_f32_e32 v100, 0x43000000, v100
	v_mul_f32_e32 v101, 0x43000000, v101
	v_mul_f32_e32 v102, 0x43000000, v102
	v_mul_f32_e32 v103, 0x43000000, v103
	ds_write_b128 v4, v[100:103]
	v_mul_f32_e32 v104, 0x43000000, v104
	v_mul_f32_e32 v105, 0x43000000, v105
	v_mul_f32_e32 v106, 0x43000000, v106
	v_mul_f32_e32 v107, 0x43000000, v107
	ds_write_b128 v4, v[104:107] offset:1024
	v_mul_f32_e32 v108, 0x43000000, v108
	v_mul_f32_e32 v109, 0x43000000, v109
	v_mul_f32_e32 v110, 0x43000000, v110
	v_mul_f32_e32 v111, 0x43000000, v111
	ds_write_b128 v4, v[108:111] offset:2048
	v_mul_f32_e32 v112, 0x43000000, v112
	v_mul_f32_e32 v113, 0x43000000, v113
	v_mul_f32_e32 v114, 0x43000000, v114
	v_mul_f32_e32 v115, 0x43000000, v115
	ds_write_b128 v4, v[112:115] offset:3072
	v_mul_f32_e32 v116, 0x43000000, v116
	v_mul_f32_e32 v117, 0x43000000, v117
	v_mul_f32_e32 v118, 0x43000000, v118
	v_mul_f32_e32 v119, 0x43000000, v119
	ds_write_b128 v4, v[116:119] offset:4096
	v_mul_f32_e32 v120, 0x43000000, v120
	v_mul_f32_e32 v121, 0x43000000, v121
	v_mul_f32_e32 v122, 0x43000000, v122
	v_mul_f32_e32 v123, 0x43000000, v123
	ds_write_b128 v4, v[120:123] offset:5120
	v_mul_f32_e32 v124, 0x43000000, v124
	v_mul_f32_e32 v125, 0x43000000, v125
	v_mul_f32_e32 v126, 0x43000000, v126
	v_mul_f32_e32 v127, 0x43000000, v127
	ds_write_b128 v4, v[124:127] offset:6144
	v_mul_f32_e32 v128, 0x43000000, v128
	v_mul_f32_e32 v129, 0x43000000, v129
	v_mul_f32_e32 v130, 0x43000000, v130
	v_mul_f32_e32 v131, 0x43000000, v131
	ds_write_b128 v4, v[128:131] offset:7168
	s_waitcnt lgkmcnt(0)
	s_barrier
; #define GAS __attribute__((address_space(1)))
; #define LAS __attribute__((address_space(3)))
; #define LDS_WAIT() asm volatile("s_waitcnt lgkmcnt(0)" ::: "memory")
; __device__ __forceinline__ unsigned pk4_fp8(float a, float b, float c, float d) {
;     a = fminf(fmaxf(a, -448.f), 448.f); b = fminf(fmaxf(b, -448.f), 448.f); c = fminf(fmaxf(c, -448.f), 448.f); d = fminf(fmaxf(d, -448.f), 448.f);
;     int w = __builtin_amdgcn_cvt_pk_fp8_f32(a, b, 0, false); w = __builtin_amdgcn_cvt_pk_fp8_f32(c, d, w, true); return (unsigned)w; }
;     const int pr = item >> 1, kb = 2 * (pr / nblk) + (item & 1), nb = pr % nblk, k0 = 64 * kb, n0 = 32 * nb;
;     const int nr = n0 + (lane & 31); const int sc = MAP == 1 ? src_col_in(nr) : nr;
;     float v[32];
; #pragma unroll
;     for (int i = 0; i < 32; ++i) v[i] = sc >= 0 ? W[(size_t)(k0 + 2 * i + (lane >> 5)) * Nsrc + sc] : 0.f;
; #pragma unroll
;     for (int i = 0; i < 32; ++i) { const int k = k0 + 2 * i + (lane >> 5); float x = v[i] * wscale; if (KS) x *= (k < ksplit ? ksA[k] : ksB[k - ksplit]); scr[(2 * i + (lane >> 5)) * 33 + (lane & 31)] = x; }
;     LDS_WAIT(); asm volatile("" ::: "memory");
;     const int c = lane & 7;
; #pragma unroll
;     for (int j = 0; j < 4; ++j) { const int n = (lane >> 3) + 8 * j; const LAS float* s = scr + (8 * c) * 33 + n;
;         const unsigned long long o = (unsigned long long)pg8::pk4_fp8(s[0 * 33], s[1 * 33], s[2 * 33], s[3 * 33]) | ((unsigned long long)pg8::pk4_fp8(s[4 * 33], s[5 * 33], s[6 * 33], s[7 * 33]) << 32);
;         *(GAS unsigned long long*)(WT + (size_t)(n0 + n) * K + k0 + 8 * c) = o; }
;     LDS_WAIT(); asm volatile("" ::: "memory");
	s_add_i32 s17, s16, 960
	s_min_u32 s17, s17, 0xfff
	s_lshr_b32 s18, s17, 5
	s_add_i32 s18, s18, 0
	s_and_b32 s19, s17, 31
	s_lshl_b32 s18, s18, 21
	s_lshl_b32 s19, s19, 9
	s_add_u32 s18, s18, s19
	s_add_u32 s12, s2, s18
	s_addc_u32 s13, s3, 0
	global_load_dwordx4 v[100:103], v10, s[12:13]
	s_add_u32 s12, s12, 0x8000
	s_addc_u32 s13, s13, 0
	global_load_dwordx4 v[104:107], v10, s[12:13]
	s_add_u32 s12, s12, 0x8000
	s_addc_u32 s13, s13, 0
	global_load_dwordx4 v[108:111], v10, s[12:13]
	s_add_u32 s12, s12, 0x8000
	s_addc_u32 s13, s13, 0
	global_load_dwordx4 v[112:115], v10, s[12:13]
	s_add_u32 s12, s12, 0x8000
	s_addc_u32 s13, s13, 0
	global_load_dwordx4 v[116:119], v10, s[12:13]
	s_add_u32 s12, s12, 0x8000
	s_addc_u32 s13, s13, 0
	global_load_dwordx4 v[120:123], v10, s[12:13]
	s_add_u32 s12, s12, 0x8000
	s_addc_u32 s13, s13, 0
	global_load_dwordx4 v[124:127], v10, s[12:13]
	s_add_u32 s12, s12, 0x8000
	s_addc_u32 s13, s13, 0
	global_load_dwordx4 v[128:131], v10, s[12:13]
	s_add_i32 s17, s16, 576
	s_min_u32 s17, s17, 0xfff
	s_lshr_b32 s18, s17, 5
	s_add_i32 s18, s18, 0
	s_and_b32 s19, s17, 31
	s_lshl_b32 s19, s19, 21
	s_lshl_b32 s18, s18, 7
	s_add_u32 s18, s18, s19
	s_add_u32 s14, s4, s18
	s_addc_u32 s15, s5, 0
	ds_read_b32 v170, v6
	ds_read_b32 v171, v6 offset:512
	ds_read_b32 v172, v6 offset:1024
	ds_read_b32 v173, v6 offset:1536
	ds_read_b32 v174, v6 offset:2048
	ds_read_b32 v175, v6 offset:2560
	ds_read_b32 v176, v6 offset:3072
	ds_read_b32 v177, v6 offset:3584
	ds_read_b32 v196, v6 offset:4096
	ds_read_b32 v197, v6 offset:4608
	ds_read_b32 v198, v6 offset:5120
	ds_read_b32 v199, v6 offset:5632
	ds_read_b32 v200, v6 offset:6144
	ds_read_b32 v201, v6 offset:6656
	ds_read_b32 v202, v6 offset:7168
	ds_read_b32 v203, v6 offset:7680
	s_waitcnt lgkmcnt(0)
	v_max_f32_e32 v170, v170, v170
	v_max_f32_e32 v171, v171, v171
	v_max_f32_e32 v172, v172, v172
	v_max_f32_e32 v173, v173, v173
	v_max_f32_e32 v174, v174, v174
	v_max_f32_e32 v175, v175, v175
	v_max_f32_e32 v176, v176, v176
	v_max_f32_e32 v177, v177, v177
	v_max_f32_e32 v196, v196, v196
	v_max_f32_e32 v197, v197, v197
	v_max_f32_e32 v198, v198, v198
	v_max_f32_e32 v199, v199, v199
	v_max_f32_e32 v200, v200, v200
	v_max_f32_e32 v201, v201, v201
	v_max_f32_e32 v202, v202, v202
	v_max_f32_e32 v203, v203, v203
	v_med3_f32 v170, v170, s20, v13
	v_med3_f32 v171, v171, s20, v13
	v_med3_f32 v172, v172, s20, v13
	v_med3_f32 v173, v173, s20, v13
	v_med3_f32 v174, v174, s20, v13
	v_med3_f32 v175, v175, s20, v13
	v_med3_f32 v176, v176, s20, v13
	v_med3_f32 v177, v177, s20, v13
	v_med3_f32 v196, v196, s20, v13
	v_med3_f32 v197, v197, s20, v13
	v_med3_f32 v198, v198, s20, v13
	v_med3_f32 v199, v199, s20, v13
	v_med3_f32 v200, v200, s20, v13
	v_med3_f32 v201, v201, s20, v13
	v_med3_f32 v202, v202, s20, v13
	v_med3_f32 v203, v203, s20, v13
	v_mov_b32_e32 v208, 0
	v_mov_b32_e32 v209, 0
	v_mov_b32_e32 v210, 0
	v_mov_b32_e32 v211, 0
	v_cvt_pk_fp8_f32 v208, v170, v171
	v_cvt_pk_fp8_f32 v209, v174, v175
	v_cvt_pk_fp8_f32 v210, v196, v197
	v_cvt_pk_fp8_f32 v211, v200, v201
	v_cvt_pk_fp8_f32 v208, v172, v173 op_sel:[0,0,1]
	v_cvt_pk_fp8_f32 v209, v176, v177 op_sel:[0,0,1]
	v_cvt_pk_fp8_f32 v210, v198, v199 op_sel:[0,0,1]
	v_cvt_pk_fp8_f32 v211, v202, v203 op_sel:[0,0,1]
	s_nop 0
	global_store_dwordx4 v11, v[208:211], s[14:15]
	ds_read_b32 v170, v8
	ds_read_b32 v171, v8 offset:512
	ds_read_b32 v172, v8 offset:1024
	ds_read_b32 v173, v8 offset:1536
	ds_read_b32 v174, v8 offset:2048
	ds_read_b32 v175, v8 offset:2560
	ds_read_b32 v176, v8 offset:3072
	ds_read_b32 v177, v8 offset:3584
	ds_read_b32 v196, v8 offset:4096
	ds_read_b32 v197, v8 offset:4608
	ds_read_b32 v198, v8 offset:5120
	ds_read_b32 v199, v8 offset:5632
	ds_read_b32 v200, v8 offset:6144
	ds_read_b32 v201, v8 offset:6656
	ds_read_b32 v202, v8 offset:7168
	ds_read_b32 v203, v8 offset:7680
	s_waitcnt lgkmcnt(0)
	v_max_f32_e32 v170, v170, v170
	v_max_f32_e32 v171, v171, v171
	v_max_f32_e32 v172, v172, v172
	v_max_f32_e32 v173, v173, v173
	v_max_f32_e32 v174, v174, v174
	v_max_f32_e32 v175, v175, v175
	v_max_f32_e32 v176, v176, v176
	v_max_f32_e32 v177, v177, v177
	v_max_f32_e32 v196, v196, v196
	v_max_f32_e32 v197, v197, v197
	v_max_f32_e32 v198, v198, v198
	v_max_f32_e32 v199, v199, v199
	v_max_f32_e32 v200, v200, v200
	v_max_f32_e32 v201, v201, v201
	v_max_f32_e32 v202, v202, v202
	v_max_f32_e32 v203, v203, v203
	v_med3_f32 v170, v170, s20, v13
	v_med3_f32 v171, v171, s20, v13
	v_med3_f32 v172, v172, s20, v13
	v_med3_f32 v173, v173, s20, v13
	v_med3_f32 v174, v174, s20, v13
	v_med3_f32 v175, v175, s20, v13
	v_med3_f32 v176, v176, s20, v13
	v_med3_f32 v177, v177, s20, v13
	v_med3_f32 v196, v196, s20, v13
	v_med3_f32 v197, v197, s20, v13
	v_med3_f32 v198, v198, s20, v13
	v_med3_f32 v199, v199, s20, v13
	v_med3_f32 v200, v200, s20, v13
	v_med3_f32 v201, v201, s20, v13
	v_med3_f32 v202, v202, s20, v13
	v_med3_f32 v203, v203, s20, v13
	v_mov_b32_e32 v208, 0
	v_mov_b32_e32 v209, 0
	v_mov_b32_e32 v210, 0
	v_mov_b32_e32 v211, 0
	v_cvt_pk_fp8_f32 v208, v170, v171
	v_cvt_pk_fp8_f32 v209, v174, v175
	v_cvt_pk_fp8_f32 v210, v196, v197
	v_cvt_pk_fp8_f32 v211, v200, v201
	v_cvt_pk_fp8_f32 v208, v172, v173 op_sel:[0,0,1]
	v_cvt_pk_fp8_f32 v209, v176, v177 op_sel:[0,0,1]
	v_cvt_pk_fp8_f32 v210, v198, v199 op_sel:[0,0,1]
	v_cvt_pk_fp8_f32 v211, v202, v203 op_sel:[0,0,1]
	s_nop 0
	global_store_dwordx4 v12, v[208:211], s[14:15]
	s_waitcnt vmcnt(32)
	v_mul_f32_e32 v132, 0x43000000, v132
	v_mul_f32_e32 v133, 0x43000000, v133
	v_mul_f32_e32 v134, 0x43000000, v134
	v_mul_f32_e32 v135, 0x43000000, v135
	ds_write_b128 v5, v[132:135]
	v_mul_f32_e32 v136, 0x43000000, v136
	v_mul_f32_e32 v137, 0x43000000, v137
	v_mul_f32_e32 v138, 0x43000000, v138
	v_mul_f32_e32 v139, 0x43000000, v139
	ds_write_b128 v5, v[136:139] offset:1024
	v_mul_f32_e32 v140, 0x43000000, v140
	v_mul_f32_e32 v141, 0x43000000, v141
	v_mul_f32_e32 v142, 0x43000000, v142
	v_mul_f32_e32 v143, 0x43000000, v143
	ds_write_b128 v5, v[140:143] offset:2048
	v_mul_f32_e32 v144, 0x43000000, v144
	v_mul_f32_e32 v145, 0x43000000, v145
	v_mul_f32_e32 v146, 0x43000000, v146
	v_mul_f32_e32 v147, 0x43000000, v147
	ds_write_b128 v5, v[144:147] offset:3072
	v_mul_f32_e32 v148, 0x43000000, v148
	v_mul_f32_e32 v149, 0x43000000, v149
	v_mul_f32_e32 v150, 0x43000000, v150
	v_mul_f32_e32 v151, 0x43000000, v151
	ds_write_b128 v5, v[148:151] offset:4096
	v_mul_f32_e32 v152, 0x43000000, v152
	v_mul_f32_e32 v153, 0x43000000, v153
	v_mul_f32_e32 v154, 0x43000000, v154
	v_mul_f32_e32 v155, 0x43000000, v155
	ds_write_b128 v5, v[152:155] offset:5120
	v_mul_f32_e32 v156, 0x43000000, v156
	v_mul_f32_e32 v157, 0x43000000, v157
	v_mul_f32_e32 v158, 0x43000000, v158
	v_mul_f32_e32 v159, 0x43000000, v159
	ds_write_b128 v5, v[156:159] offset:6144
	v_mul_f32_e32 v160, 0x43000000, v160
	v_mul_f32_e32 v161, 0x43000000, v161
	v_mul_f32_e32 v162, 0x43000000, v162
	v_mul_f32_e32 v163, 0x43000000, v163
	ds_write_b128 v5, v[160:163] offset:7168
	s_waitcnt lgkmcnt(0)
	s_barrier
; #define GAS __attribute__((address_space(1)))
; #define LAS __attribute__((address_space(3)))
; #define LDS_WAIT() asm volatile("s_waitcnt lgkmcnt(0)" ::: "memory")
; __device__ __forceinline__ unsigned pk4_fp8(float a, float b, float c, float d) {
;     a = fminf(fmaxf(a, -448.f), 448.f); b = fminf(fmaxf(b, -448.f), 448.f); c = fminf(fmaxf(c, -448.f), 448.f); d = fminf(fmaxf(d, -448.f), 448.f);
;     int w = __builtin_amdgcn_cvt_pk_fp8_f32(a, b, 0, false); w = __builtin_amdgcn_cvt_pk_fp8_f32(c, d, w, true); return (unsigned)w; }
;     const int pr = item >> 1, kb = 2 * (pr / nblk) + (item & 1), nb = pr % nblk, k0 = 64 * kb, n0 = 32 * nb;
;     const int nr = n0 + (lane & 31); const int sc = MAP == 1 ? src_col_in(nr) : nr;
;     float v[32];
; #pragma unroll
;     for (int i = 0; i < 32; ++i) v[i] = sc >= 0 ? W[(size_t)(k0 + 2 * i + (lane >> 5)) * Nsrc + sc] : 0.f;
; #pragma unroll
;     for (int i = 0; i < 32; ++i) { const int k = k0 + 2 * i + (lane >> 5); float x = v[i] * wscale; if (KS) x *= (k < ksplit ? ksA[k] : ksB[k - ksplit]); scr[(2 * i + (lane >> 5)) * 33 + (lane & 31)] = x; }
;     LDS_WAIT(); asm volatile("" ::: "memory");
;     const int c = lane & 7;
; #pragma unroll
;     for (int j = 0; j < 4; ++j) { const int n = (lane >> 3) + 8 * j; const LAS float* s = scr + (8 * c) * 33 + n;
;         const unsigned long long o = (unsigned long long)pg8::pk4_fp8(s[0 * 33], s[1 * 33], s[2 * 33], s[3 * 33]) | ((unsigned long long)pg8::pk4_fp8(s[4 * 33], s[5 * 33], s[6 * 33], s[7 * 33]) << 32);
;         *(GAS unsigned long long*)(WT + (size_t)(n0 + n) * K + k0 + 8 * c) = o; }
;     LDS_WAIT(); asm volatile("" ::: "memory");
	s_add_i32 s17, s16, 1056
	s_min_u32 s17, s17, 0xfff
	s_lshr_b32 s18, s17, 5
	s_add_i32 s18, s18, 0
	s_and_b32 s19, s17, 31
	s_lshl_b32 s18, s18, 21
	s_lshl_b32 s19, s19, 9
	s_add_u32 s18, s18, s19
	s_add_u32 s12, s2, s18
	s_addc_u32 s13, s3, 0
	global_load_dwordx4 v[132:135], v10, s[12:13]
	s_add_u32 s12, s12, 0x8000
	s_addc_u32 s13, s13, 0
	global_load_dwordx4 v[136:139], v10, s[12:13]
	s_add_u32 s12, s12, 0x8000
	s_addc_u32 s13, s13, 0
	global_load_dwordx4 v[140:143], v10, s[12:13]
	s_add_u32 s12, s12, 0x8000
	s_addc_u32 s13, s13, 0
	global_load_dwordx4 v[144:147], v10, s[12:13]
	s_add_u32 s12, s12, 0x8000
	s_addc_u32 s13, s13, 0
	global_load_dwordx4 v[148:151], v10, s[12:13]
	s_add_u32 s12, s12, 0x8000
	s_addc_u32 s13, s13, 0
	global_load_dwordx4 v[152:155], v10, s[12:13]
	s_add_u32 s12, s12, 0x8000
	s_addc_u32 s13, s13, 0
	global_load_dwordx4 v[156:159], v10, s[12:13]
	s_add_u32 s12, s12, 0x8000
	s_addc_u32 s13, s13, 0
	global_load_dwordx4 v[160:163], v10, s[12:13]
	s_add_i32 s17, s16, 672
	s_min_u32 s17, s17, 0xfff
	s_lshr_b32 s18, s17, 5
	s_add_i32 s18, s18, 0
	s_and_b32 s19, s17, 31
	s_lshl_b32 s19, s19, 21
	s_lshl_b32 s18, s18, 7
	s_add_u32 s18, s18, s19
	s_add_u32 s14, s4, s18
	s_addc_u32 s15, s5, 0
	ds_read_b32 v170, v7
	ds_read_b32 v171, v7 offset:512
	ds_read_b32 v172, v7 offset:1024
	ds_read_b32 v173, v7 offset:1536
	ds_read_b32 v174, v7 offset:2048
	ds_read_b32 v175, v7 offset:2560
	ds_read_b32 v176, v7 offset:3072
	ds_read_b32 v177, v7 offset:3584
	ds_read_b32 v196, v7 offset:4096
	ds_read_b32 v197, v7 offset:4608
	ds_read_b32 v198, v7 offset:5120
	ds_read_b32 v199, v7 offset:5632
	ds_read_b32 v200, v7 offset:6144
	ds_read_b32 v201, v7 offset:6656
	ds_read_b32 v202, v7 offset:7168
	ds_read_b32 v203, v7 offset:7680
	s_waitcnt lgkmcnt(0)
	v_max_f32_e32 v170, v170, v170
	v_max_f32_e32 v171, v171, v171
	v_max_f32_e32 v172, v172, v172
	v_max_f32_e32 v173, v173, v173
	v_max_f32_e32 v174, v174, v174
	v_max_f32_e32 v175, v175, v175
	v_max_f32_e32 v176, v176, v176
	v_max_f32_e32 v177, v177, v177
	v_max_f32_e32 v196, v196, v196
	v_max_f32_e32 v197, v197, v197
	v_max_f32_e32 v198, v198, v198
	v_max_f32_e32 v199, v199, v199
	v_max_f32_e32 v200, v200, v200
	v_max_f32_e32 v201, v201, v201
	v_max_f32_e32 v202, v202, v202
	v_max_f32_e32 v203, v203, v203
	v_med3_f32 v170, v170, s20, v13
	v_med3_f32 v171, v171, s20, v13
	v_med3_f32 v172, v172, s20, v13
	v_med3_f32 v173, v173, s20, v13
	v_med3_f32 v174, v174, s20, v13
	v_med3_f32 v175, v175, s20, v13
	v_med3_f32 v176, v176, s20, v13
	v_med3_f32 v177, v177, s20, v13
	v_med3_f32 v196, v196, s20, v13
	v_med3_f32 v197, v197, s20, v13
	v_med3_f32 v198, v198, s20, v13
	v_med3_f32 v199, v199, s20, v13
	v_med3_f32 v200, v200, s20, v13
	v_med3_f32 v201, v201, s20, v13
	v_med3_f32 v202, v202, s20, v13
	v_med3_f32 v203, v203, s20, v13
	v_mov_b32_e32 v208, 0
	v_mov_b32_e32 v209, 0
	v_mov_b32_e32 v210, 0
	v_mov_b32_e32 v211, 0
	v_cvt_pk_fp8_f32 v208, v170, v171
	v_cvt_pk_fp8_f32 v209, v174, v175
	v_cvt_pk_fp8_f32 v210, v196, v197
	v_cvt_pk_fp8_f32 v211, v200, v201
	v_cvt_pk_fp8_f32 v208, v172, v173 op_sel:[0,0,1]
	v_cvt_pk_fp8_f32 v209, v176, v177 op_sel:[0,0,1]
	v_cvt_pk_fp8_f32 v210, v198, v199 op_sel:[0,0,1]
	v_cvt_pk_fp8_f32 v211, v202, v203 op_sel:[0,0,1]
	s_nop 0
	global_store_dwordx4 v11, v[208:211], s[14:15]
	ds_read_b32 v170, v9
	ds_read_b32 v171, v9 offset:512
	ds_read_b32 v172, v9 offset:1024
	ds_read_b32 v173, v9 offset:1536
	ds_read_b32 v174, v9 offset:2048
	ds_read_b32 v175, v9 offset:2560
	ds_read_b32 v176, v9 offset:3072
	ds_read_b32 v177, v9 offset:3584
	ds_read_b32 v196, v9 offset:4096
	ds_read_b32 v197, v9 offset:4608
	ds_read_b32 v198, v9 offset:5120
	ds_read_b32 v199, v9 offset:5632
	ds_read_b32 v200, v9 offset:6144
	ds_read_b32 v201, v9 offset:6656
	ds_read_b32 v202, v9 offset:7168
	ds_read_b32 v203, v9 offset:7680
	s_waitcnt lgkmcnt(0)
	v_max_f32_e32 v170, v170, v170
	v_max_f32_e32 v171, v171, v171
	v_max_f32_e32 v172, v172, v172
	v_max_f32_e32 v173, v173, v173
	v_max_f32_e32 v174, v174, v174
	v_max_f32_e32 v175, v175, v175
	v_max_f32_e32 v176, v176, v176
	v_max_f32_e32 v177, v177, v177
	v_max_f32_e32 v196, v196, v196
	v_max_f32_e32 v197, v197, v197
	v_max_f32_e32 v198, v198, v198
	v_max_f32_e32 v199, v199, v199
	v_max_f32_e32 v200, v200, v200
	v_max_f32_e32 v201, v201, v201
	v_max_f32_e32 v202, v202, v202
	v_max_f32_e32 v203, v203, v203
	v_med3_f32 v170, v170, s20, v13
	v_med3_f32 v171, v171, s20, v13
	v_med3_f32 v172, v172, s20, v13
	v_med3_f32 v173, v173, s20, v13
	v_med3_f32 v174, v174, s20, v13
	v_med3_f32 v175, v175, s20, v13
	v_med3_f32 v176, v176, s20, v13
	v_med3_f32 v177, v177, s20, v13
	v_med3_f32 v196, v196, s20, v13
	v_med3_f32 v197, v197, s20, v13
	v_med3_f32 v198, v198, s20, v13
	v_med3_f32 v199, v199, s20, v13
	v_med3_f32 v200, v200, s20, v13
	v_med3_f32 v201, v201, s20, v13
	v_med3_f32 v202, v202, s20, v13
	v_med3_f32 v203, v203, s20, v13
	v_mov_b32_e32 v208, 0
	v_mov_b32_e32 v209, 0
	v_mov_b32_e32 v210, 0
	v_mov_b32_e32 v211, 0
	v_cvt_pk_fp8_f32 v208, v170, v171
	v_cvt_pk_fp8_f32 v209, v174, v175
	v_cvt_pk_fp8_f32 v210, v196, v197
	v_cvt_pk_fp8_f32 v211, v200, v201
	v_cvt_pk_fp8_f32 v208, v172, v173 op_sel:[0,0,1]
	v_cvt_pk_fp8_f32 v209, v176, v177 op_sel:[0,0,1]
	v_cvt_pk_fp8_f32 v210, v198, v199 op_sel:[0,0,1]
	v_cvt_pk_fp8_f32 v211, v202, v203 op_sel:[0,0,1]
	s_nop 0
	global_store_dwordx4 v12, v[208:211], s[14:15]
	s_waitcnt vmcnt(32)
	v_mul_f32_e32 v36, 0x43000000, v36
	v_mul_f32_e32 v37, 0x43000000, v37
	v_mul_f32_e32 v38, 0x43000000, v38
	v_mul_f32_e32 v39, 0x43000000, v39
	ds_write_b128 v4, v[36:39]
	v_mul_f32_e32 v40, 0x43000000, v40
	v_mul_f32_e32 v41, 0x43000000, v41
	v_mul_f32_e32 v42, 0x43000000, v42
	v_mul_f32_e32 v43, 0x43000000, v43
	ds_write_b128 v4, v[40:43] offset:1024
	v_mul_f32_e32 v44, 0x43000000, v44
	v_mul_f32_e32 v45, 0x43000000, v45
	v_mul_f32_e32 v46, 0x43000000, v46
	v_mul_f32_e32 v47, 0x43000000, v47
	ds_write_b128 v4, v[44:47] offset:2048
	v_mul_f32_e32 v48, 0x43000000, v48
	v_mul_f32_e32 v49, 0x43000000, v49
	v_mul_f32_e32 v50, 0x43000000, v50
	v_mul_f32_e32 v51, 0x43000000, v51
	ds_write_b128 v4, v[48:51] offset:3072
	v_mul_f32_e32 v52, 0x43000000, v52
	v_mul_f32_e32 v53, 0x43000000, v53
	v_mul_f32_e32 v54, 0x43000000, v54
	v_mul_f32_e32 v55, 0x43000000, v55
	ds_write_b128 v4, v[52:55] offset:4096
	v_mul_f32_e32 v56, 0x43000000, v56
	v_mul_f32_e32 v57, 0x43000000, v57
	v_mul_f32_e32 v58, 0x43000000, v58
	v_mul_f32_e32 v59, 0x43000000, v59
	ds_write_b128 v4, v[56:59] offset:5120
	v_mul_f32_e32 v60, 0x43000000, v60
	v_mul_f32_e32 v61, 0x43000000, v61
	v_mul_f32_e32 v62, 0x43000000, v62
	v_mul_f32_e32 v63, 0x43000000, v63
	ds_write_b128 v4, v[60:63] offset:6144
	v_mul_f32_e32 v64, 0x43000000, v64
	v_mul_f32_e32 v65, 0x43000000, v65
	v_mul_f32_e32 v66, 0x43000000, v66
	v_mul_f32_e32 v67, 0x43000000, v67
	ds_write_b128 v4, v[64:67] offset:7168
	s_waitcnt lgkmcnt(0)
	s_barrier
; #define GAS __attribute__((address_space(1)))
; #define LAS __attribute__((address_space(3)))
; #define LDS_WAIT() asm volatile("s_waitcnt lgkmcnt(0)" ::: "memory")
; __device__ __forceinline__ unsigned pk4_fp8(float a, float b, float c, float d) {
;     a = fminf(fmaxf(a, -448.f), 448.f); b = fminf(fmaxf(b, -448.f), 448.f); c = fminf(fmaxf(c, -448.f), 448.f); d = fminf(fmaxf(d, -448.f), 448.f);
;     int w = __builtin_amdgcn_cvt_pk_fp8_f32(a, b, 0, false); w = __builtin_amdgcn_cvt_pk_fp8_f32(c, d, w, true); return (unsigned)w; }
;     const int pr = item >> 1, kb = 2 * (pr / nblk) + (item & 1), nb = pr % nblk, k0 = 64 * kb, n0 = 32 * nb;
;     const int nr = n0 + (lane & 31); const int sc = MAP == 1 ? src_col_in(nr) : nr;
;     float v[32];
; #pragma unroll
;     for (int i = 0; i < 32; ++i) v[i] = sc >= 0 ? W[(size_t)(k0 + 2 * i + (lane >> 5)) * Nsrc + sc] : 0.f;
; #pragma unroll
;     for (int i = 0; i < 32; ++i) { const int k = k0 + 2 * i + (lane >> 5); float x = v[i] * wscale; if (KS) x *= (k < ksplit ? ksA[k] : ksB[k - ksplit]); scr[(2 * i + (lane >> 5)) * 33 + (lane & 31)] = x; }
;     LDS_WAIT(); asm volatile("" ::: "memory");
;     const int c = lane & 7;
; #pragma unroll
;     for (int j = 0; j < 4; ++j) { const int n = (lane >> 3) + 8 * j; const LAS float* s = scr + (8 * c) * 33 + n;
;         const unsigned long long o = (unsigned long long)pg8::pk4_fp8(s[0 * 33], s[1 * 33], s[2 * 33], s[3 * 33]) | ((unsigned long long)pg8::pk4_fp8(s[4 * 33], s[5 * 33], s[6 * 33], s[7 * 33]) << 32);
;         *(GAS unsigned long long*)(WT + (size_t)(n0 + n) * K + k0 + 8 * c) = o; }
;     LDS_WAIT(); asm volatile("" ::: "memory");
	s_add_i32 s17, s16, 1152
	s_min_u32 s17, s17, 0xfff
	s_lshr_b32 s18, s17, 5
	s_add_i32 s18, s18, 0
	s_and_b32 s19, s17, 31
	s_lshl_b32 s18, s18, 21
	s_lshl_b32 s19, s19, 9
	s_add_u32 s18, s18, s19
	s_add_u32 s12, s2, s18
	s_addc_u32 s13, s3, 0
	global_load_dwordx4 v[36:39], v10, s[12:13]
	s_add_u32 s12, s12, 0x8000
	s_addc_u32 s13, s13, 0
	global_load_dwordx4 v[40:43], v10, s[12:13]
	s_add_u32 s12, s12, 0x8000
	s_addc_u32 s13, s13, 0
	global_load_dwordx4 v[44:47], v10, s[12:13]
	s_add_u32 s12, s12, 0x8000
	s_addc_u32 s13, s13, 0
	global_load_dwordx4 v[48:51], v10, s[12:13]
	s_add_u32 s12, s12, 0x8000
	s_addc_u32 s13, s13, 0
	global_load_dwordx4 v[52:55], v10, s[12:13]
	s_add_u32 s12, s12, 0x8000
	s_addc_u32 s13, s13, 0
	global_load_dwordx4 v[56:59], v10, s[12:13]
	s_add_u32 s12, s12, 0x8000
	s_addc_u32 s13, s13, 0
	global_load_dwordx4 v[60:63], v10, s[12:13]
	s_add_u32 s12, s12, 0x8000
	s_addc_u32 s13, s13, 0
	global_load_dwordx4 v[64:67], v10, s[12:13]
	s_add_i32 s17, s16, 768
	s_min_u32 s17, s17, 0xfff
	s_lshr_b32 s18, s17, 5
	s_add_i32 s18, s18, 0
	s_and_b32 s19, s17, 31
	s_lshl_b32 s19, s19, 21
	s_lshl_b32 s18, s18, 7
	s_add_u32 s18, s18, s19
	s_add_u32 s14, s4, s18
	s_addc_u32 s15, s5, 0
	ds_read_b32 v170, v6
	ds_read_b32 v171, v6 offset:512
	ds_read_b32 v172, v6 offset:1024
	ds_read_b32 v173, v6 offset:1536
	ds_read_b32 v174, v6 offset:2048
	ds_read_b32 v175, v6 offset:2560
	ds_read_b32 v176, v6 offset:3072
	ds_read_b32 v177, v6 offset:3584
	ds_read_b32 v196, v6 offset:4096
	ds_read_b32 v197, v6 offset:4608
	ds_read_b32 v198, v6 offset:5120
	ds_read_b32 v199, v6 offset:5632
	ds_read_b32 v200, v6 offset:6144
	ds_read_b32 v201, v6 offset:6656
	ds_read_b32 v202, v6 offset:7168
	ds_read_b32 v203, v6 offset:7680
	s_waitcnt lgkmcnt(0)
	v_max_f32_e32 v170, v170, v170
	v_max_f32_e32 v171, v171, v171
	v_max_f32_e32 v172, v172, v172
	v_max_f32_e32 v173, v173, v173
	v_max_f32_e32 v174, v174, v174
	v_max_f32_e32 v175, v175, v175
	v_max_f32_e32 v176, v176, v176
	v_max_f32_e32 v177, v177, v177
	v_max_f32_e32 v196, v196, v196
	v_max_f32_e32 v197, v197, v197
	v_max_f32_e32 v198, v198, v198
	v_max_f32_e32 v199, v199, v199
	v_max_f32_e32 v200, v200, v200
	v_max_f32_e32 v201, v201, v201
	v_max_f32_e32 v202, v202, v202
	v_max_f32_e32 v203, v203, v203
	v_med3_f32 v170, v170, s20, v13
	v_med3_f32 v171, v171, s20, v13
	v_med3_f32 v172, v172, s20, v13
	v_med3_f32 v173, v173, s20, v13
	v_med3_f32 v174, v174, s20, v13
	v_med3_f32 v175, v175, s20, v13
	v_med3_f32 v176, v176, s20, v13
	v_med3_f32 v177, v177, s20, v13
	v_med3_f32 v196, v196, s20, v13
	v_med3_f32 v197, v197, s20, v13
	v_med3_f32 v198, v198, s20, v13
	v_med3_f32 v199, v199, s20, v13
	v_med3_f32 v200, v200, s20, v13
	v_med3_f32 v201, v201, s20, v13
	v_med3_f32 v202, v202, s20, v13
	v_med3_f32 v203, v203, s20, v13
	v_mov_b32_e32 v208, 0
	v_mov_b32_e32 v209, 0
	v_mov_b32_e32 v210, 0
	v_mov_b32_e32 v211, 0
	v_cvt_pk_fp8_f32 v208, v170, v171
	v_cvt_pk_fp8_f32 v209, v174, v175
	v_cvt_pk_fp8_f32 v210, v196, v197
	v_cvt_pk_fp8_f32 v211, v200, v201
	v_cvt_pk_fp8_f32 v208, v172, v173 op_sel:[0,0,1]
	v_cvt_pk_fp8_f32 v209, v176, v177 op_sel:[0,0,1]
	v_cvt_pk_fp8_f32 v210, v198, v199 op_sel:[0,0,1]
	v_cvt_pk_fp8_f32 v211, v202, v203 op_sel:[0,0,1]
	s_nop 0
	global_store_dwordx4 v11, v[208:211], s[14:15]
	ds_read_b32 v170, v8
	ds_read_b32 v171, v8 offset:512
	ds_read_b32 v172, v8 offset:1024
	ds_read_b32 v173, v8 offset:1536
	ds_read_b32 v174, v8 offset:2048
	ds_read_b32 v175, v8 offset:2560
	ds_read_b32 v176, v8 offset:3072
	ds_read_b32 v177, v8 offset:3584
	ds_read_b32 v196, v8 offset:4096
	ds_read_b32 v197, v8 offset:4608
	ds_read_b32 v198, v8 offset:5120
	ds_read_b32 v199, v8 offset:5632
	ds_read_b32 v200, v8 offset:6144
	ds_read_b32 v201, v8 offset:6656
	ds_read_b32 v202, v8 offset:7168
	ds_read_b32 v203, v8 offset:7680
	s_waitcnt lgkmcnt(0)
	v_max_f32_e32 v170, v170, v170
	v_max_f32_e32 v171, v171, v171
	v_max_f32_e32 v172, v172, v172
	v_max_f32_e32 v173, v173, v173
	v_max_f32_e32 v174, v174, v174
	v_max_f32_e32 v175, v175, v175
	v_max_f32_e32 v176, v176, v176
	v_max_f32_e32 v177, v177, v177
	v_max_f32_e32 v196, v196, v196
	v_max_f32_e32 v197, v197, v197
	v_max_f32_e32 v198, v198, v198
	v_max_f32_e32 v199, v199, v199
	v_max_f32_e32 v200, v200, v200
	v_max_f32_e32 v201, v201, v201
	v_max_f32_e32 v202, v202, v202
	v_max_f32_e32 v203, v203, v203
	v_med3_f32 v170, v170, s20, v13
	v_med3_f32 v171, v171, s20, v13
	v_med3_f32 v172, v172, s20, v13
	v_med3_f32 v173, v173, s20, v13
	v_med3_f32 v174, v174, s20, v13
	v_med3_f32 v175, v175, s20, v13
	v_med3_f32 v176, v176, s20, v13
	v_med3_f32 v177, v177, s20, v13
	v_med3_f32 v196, v196, s20, v13
	v_med3_f32 v197, v197, s20, v13
	v_med3_f32 v198, v198, s20, v13
	v_med3_f32 v199, v199, s20, v13
	v_med3_f32 v200, v200, s20, v13
	v_med3_f32 v201, v201, s20, v13
	v_med3_f32 v202, v202, s20, v13
	v_med3_f32 v203, v203, s20, v13
	v_mov_b32_e32 v208, 0
	v_mov_b32_e32 v209, 0
	v_mov_b32_e32 v210, 0
	v_mov_b32_e32 v211, 0
	v_cvt_pk_fp8_f32 v208, v170, v171
	v_cvt_pk_fp8_f32 v209, v174, v175
	v_cvt_pk_fp8_f32 v210, v196, v197
	v_cvt_pk_fp8_f32 v211, v200, v201
	v_cvt_pk_fp8_f32 v208, v172, v173 op_sel:[0,0,1]
	v_cvt_pk_fp8_f32 v209, v176, v177 op_sel:[0,0,1]
	v_cvt_pk_fp8_f32 v210, v198, v199 op_sel:[0,0,1]
	v_cvt_pk_fp8_f32 v211, v202, v203 op_sel:[0,0,1]
	s_nop 0
	global_store_dwordx4 v12, v[208:211], s[14:15]
	s_waitcnt vmcnt(32)
	v_mul_f32_e32 v68, 0x43000000, v68
	v_mul_f32_e32 v69, 0x43000000, v69
	v_mul_f32_e32 v70, 0x43000000, v70
	v_mul_f32_e32 v71, 0x43000000, v71
	ds_write_b128 v5, v[68:71]
	v_mul_f32_e32 v72, 0x43000000, v72
	v_mul_f32_e32 v73, 0x43000000, v73
	v_mul_f32_e32 v74, 0x43000000, v74
	v_mul_f32_e32 v75, 0x43000000, v75
	ds_write_b128 v5, v[72:75] offset:1024
	v_mul_f32_e32 v76, 0x43000000, v76
	v_mul_f32_e32 v77, 0x43000000, v77
	v_mul_f32_e32 v78, 0x43000000, v78
	v_mul_f32_e32 v79, 0x43000000, v79
	ds_write_b128 v5, v[76:79] offset:2048
	v_mul_f32_e32 v80, 0x43000000, v80
	v_mul_f32_e32 v81, 0x43000000, v81
	v_mul_f32_e32 v82, 0x43000000, v82
	v_mul_f32_e32 v83, 0x43000000, v83
	ds_write_b128 v5, v[80:83] offset:3072
	v_mul_f32_e32 v84, 0x43000000, v84
	v_mul_f32_e32 v85, 0x43000000, v85
	v_mul_f32_e32 v86, 0x43000000, v86
	v_mul_f32_e32 v87, 0x43000000, v87
	ds_write_b128 v5, v[84:87] offset:4096
	v_mul_f32_e32 v88, 0x43000000, v88
	v_mul_f32_e32 v89, 0x43000000, v89
	v_mul_f32_e32 v90, 0x43000000, v90
	v_mul_f32_e32 v91, 0x43000000, v91
	ds_write_b128 v5, v[88:91] offset:5120
	v_mul_f32_e32 v92, 0x43000000, v92
	v_mul_f32_e32 v93, 0x43000000, v93
	v_mul_f32_e32 v94, 0x43000000, v94
	v_mul_f32_e32 v95, 0x43000000, v95
	ds_write_b128 v5, v[92:95] offset:6144
	v_mul_f32_e32 v96, 0x43000000, v96
	v_mul_f32_e32 v97, 0x43000000, v97
	v_mul_f32_e32 v98, 0x43000000, v98
	v_mul_f32_e32 v99, 0x43000000, v99
	ds_write_b128 v5, v[96:99] offset:7168
	s_waitcnt lgkmcnt(0)
	s_barrier
; #define GAS __attribute__((address_space(1)))
; #define LAS __attribute__((address_space(3)))
; #define LDS_WAIT() asm volatile("s_waitcnt lgkmcnt(0)" ::: "memory")
; __device__ __forceinline__ unsigned pk4_fp8(float a, float b, float c, float d) {
;     a = fminf(fmaxf(a, -448.f), 448.f); b = fminf(fmaxf(b, -448.f), 448.f); c = fminf(fmaxf(c, -448.f), 448.f); d = fminf(fmaxf(d, -448.f), 448.f);
;     int w = __builtin_amdgcn_cvt_pk_fp8_f32(a, b, 0, false); w = __builtin_amdgcn_cvt_pk_fp8_f32(c, d, w, true); return (unsigned)w; }
;     const int pr = item >> 1, kb = 2 * (pr / nblk) + (item & 1), nb = pr % nblk, k0 = 64 * kb, n0 = 32 * nb;
;     const int nr = n0 + (lane & 31); const int sc = MAP == 1 ? src_col_in(nr) : nr;
;     float v[32];
; #pragma unroll
;     for (int i = 0; i < 32; ++i) v[i] = sc >= 0 ? W[(size_t)(k0 + 2 * i + (lane >> 5)) * Nsrc + sc] : 0.f;
; #pragma unroll
;     for (int i = 0; i < 32; ++i) { const int k = k0 + 2 * i + (lane >> 5); float x = v[i] * wscale; if (KS) x *= (k < ksplit ? ksA[k] : ksB[k - ksplit]); scr[(2 * i + (lane >> 5)) * 33 + (lane & 31)] = x; }
;     LDS_WAIT(); asm volatile("" ::: "memory");
;     const int c = lane & 7;
; #pragma unroll
;     for (int j = 0; j < 4; ++j) { const int n = (lane >> 3) + 8 * j; const LAS float* s = scr + (8 * c) * 33 + n;
;         const unsigned long long o = (unsigned long long)pg8::pk4_fp8(s[0 * 33], s[1 * 33], s[2 * 33], s[3 * 33]) | ((unsigned long long)pg8::pk4_fp8(s[4 * 33], s[5 * 33], s[6 * 33], s[7 * 33]) << 32);
;         *(GAS unsigned long long*)(WT + (size_t)(n0 + n) * K + k0 + 8 * c) = o; }
;     LDS_WAIT(); asm volatile("" ::: "memory");
	s_add_i32 s17, s16, 1248
	s_min_u32 s17, s17, 0xfff
	s_lshr_b32 s18, s17, 5
	s_add_i32 s18, s18, 0
	s_and_b32 s19, s17, 31
	s_lshl_b32 s18, s18, 21
	s_lshl_b32 s19, s19, 9
	s_add_u32 s18, s18, s19
	s_add_u32 s12, s2, s18
	s_addc_u32 s13, s3, 0
	global_load_dwordx4 v[68:71], v10, s[12:13]
	s_add_u32 s12, s12, 0x8000
	s_addc_u32 s13, s13, 0
	global_load_dwordx4 v[72:75], v10, s[12:13]
	s_add_u32 s12, s12, 0x8000
	s_addc_u32 s13, s13, 0
	global_load_dwordx4 v[76:79], v10, s[12:13]
	s_add_u32 s12, s12, 0x8000
	s_addc_u32 s13, s13, 0
	global_load_dwordx4 v[80:83], v10, s[12:13]
	s_add_u32 s12, s12, 0x8000
	s_addc_u32 s13, s13, 0
	global_load_dwordx4 v[84:87], v10, s[12:13]
	s_add_u32 s12, s12, 0x8000
	s_addc_u32 s13, s13, 0
	global_load_dwordx4 v[88:91], v10, s[12:13]
	s_add_u32 s12, s12, 0x8000
	s_addc_u32 s13, s13, 0
	global_load_dwordx4 v[92:95], v10, s[12:13]
	s_add_u32 s12, s12, 0x8000
	s_addc_u32 s13, s13, 0
	global_load_dwordx4 v[96:99], v10, s[12:13]
	s_add_i32 s17, s16, 864
	s_min_u32 s17, s17, 0xfff
	s_lshr_b32 s18, s17, 5
	s_add_i32 s18, s18, 0
	s_and_b32 s19, s17, 31
	s_lshl_b32 s19, s19, 21
	s_lshl_b32 s18, s18, 7
	s_add_u32 s18, s18, s19
	s_add_u32 s14, s4, s18
	s_addc_u32 s15, s5, 0
	ds_read_b32 v170, v7
	ds_read_b32 v171, v7 offset:512
	ds_read_b32 v172, v7 offset:1024
	ds_read_b32 v173, v7 offset:1536
	ds_read_b32 v174, v7 offset:2048
	ds_read_b32 v175, v7 offset:2560
	ds_read_b32 v176, v7 offset:3072
	ds_read_b32 v177, v7 offset:3584
	ds_read_b32 v196, v7 offset:4096
	ds_read_b32 v197, v7 offset:4608
	ds_read_b32 v198, v7 offset:5120
	ds_read_b32 v199, v7 offset:5632
	ds_read_b32 v200, v7 offset:6144
	ds_read_b32 v201, v7 offset:6656
	ds_read_b32 v202, v7 offset:7168
	ds_read_b32 v203, v7 offset:7680
	s_waitcnt lgkmcnt(0)
	v_max_f32_e32 v170, v170, v170
	v_max_f32_e32 v171, v171, v171
	v_max_f32_e32 v172, v172, v172
	v_max_f32_e32 v173, v173, v173
	v_max_f32_e32 v174, v174, v174
	v_max_f32_e32 v175, v175, v175
	v_max_f32_e32 v176, v176, v176
	v_max_f32_e32 v177, v177, v177
	v_max_f32_e32 v196, v196, v196
	v_max_f32_e32 v197, v197, v197
	v_max_f32_e32 v198, v198, v198
	v_max_f32_e32 v199, v199, v199
	v_max_f32_e32 v200, v200, v200
	v_max_f32_e32 v201, v201, v201
	v_max_f32_e32 v202, v202, v202
	v_max_f32_e32 v203, v203, v203
	v_med3_f32 v170, v170, s20, v13
	v_med3_f32 v171, v171, s20, v13
	v_med3_f32 v172, v172, s20, v13
	v_med3_f32 v173, v173, s20, v13
	v_med3_f32 v174, v174, s20, v13
	v_med3_f32 v175, v175, s20, v13
	v_med3_f32 v176, v176, s20, v13
	v_med3_f32 v177, v177, s20, v13
	v_med3_f32 v196, v196, s20, v13
	v_med3_f32 v197, v197, s20, v13
	v_med3_f32 v198, v198, s20, v13
	v_med3_f32 v199, v199, s20, v13
	v_med3_f32 v200, v200, s20, v13
	v_med3_f32 v201, v201, s20, v13
	v_med3_f32 v202, v202, s20, v13
	v_med3_f32 v203, v203, s20, v13
	v_mov_b32_e32 v208, 0
	v_mov_b32_e32 v209, 0
	v_mov_b32_e32 v210, 0
	v_mov_b32_e32 v211, 0
	v_cvt_pk_fp8_f32 v208, v170, v171
	v_cvt_pk_fp8_f32 v209, v174, v175
	v_cvt_pk_fp8_f32 v210, v196, v197
	v_cvt_pk_fp8_f32 v211, v200, v201
	v_cvt_pk_fp8_f32 v208, v172, v173 op_sel:[0,0,1]
	v_cvt_pk_fp8_f32 v209, v176, v177 op_sel:[0,0,1]
	v_cvt_pk_fp8_f32 v210, v198, v199 op_sel:[0,0,1]
	v_cvt_pk_fp8_f32 v211, v202, v203 op_sel:[0,0,1]
	s_nop 0
	global_store_dwordx4 v11, v[208:211], s[14:15]
	ds_read_b32 v170, v9
	ds_read_b32 v171, v9 offset:512
	ds_read_b32 v172, v9 offset:1024
	ds_read_b32 v173, v9 offset:1536
	ds_read_b32 v174, v9 offset:2048
	ds_read_b32 v175, v9 offset:2560
	ds_read_b32 v176, v9 offset:3072
	ds_read_b32 v177, v9 offset:3584
	ds_read_b32 v196, v9 offset:4096
	ds_read_b32 v197, v9 offset:4608
	ds_read_b32 v198, v9 offset:5120
	ds_read_b32 v199, v9 offset:5632
	ds_read_b32 v200, v9 offset:6144
	ds_read_b32 v201, v9 offset:6656
	ds_read_b32 v202, v9 offset:7168
	ds_read_b32 v203, v9 offset:7680
	s_waitcnt lgkmcnt(0)
	v_max_f32_e32 v170, v170, v170
	v_max_f32_e32 v171, v171, v171
	v_max_f32_e32 v172, v172, v172
	v_max_f32_e32 v173, v173, v173
	v_max_f32_e32 v174, v174, v174
	v_max_f32_e32 v175, v175, v175
	v_max_f32_e32 v176, v176, v176
	v_max_f32_e32 v177, v177, v177
	v_max_f32_e32 v196, v196, v196
	v_max_f32_e32 v197, v197, v197
	v_max_f32_e32 v198, v198, v198
	v_max_f32_e32 v199, v199, v199
	v_max_f32_e32 v200, v200, v200
	v_max_f32_e32 v201, v201, v201
	v_max_f32_e32 v202, v202, v202
	v_max_f32_e32 v203, v203, v203
	v_med3_f32 v170, v170, s20, v13
	v_med3_f32 v171, v171, s20, v13
	v_med3_f32 v172, v172, s20, v13
	v_med3_f32 v173, v173, s20, v13
	v_med3_f32 v174, v174, s20, v13
	v_med3_f32 v175, v175, s20, v13
	v_med3_f32 v176, v176, s20, v13
	v_med3_f32 v177, v177, s20, v13
	v_med3_f32 v196, v196, s20, v13
	v_med3_f32 v197, v197, s20, v13
	v_med3_f32 v198, v198, s20, v13
	v_med3_f32 v199, v199, s20, v13
	v_med3_f32 v200, v200, s20, v13
	v_med3_f32 v201, v201, s20, v13
	v_med3_f32 v202, v202, s20, v13
	v_med3_f32 v203, v203, s20, v13
	v_mov_b32_e32 v208, 0
	v_mov_b32_e32 v209, 0
	v_mov_b32_e32 v210, 0
	v_mov_b32_e32 v211, 0
	v_cvt_pk_fp8_f32 v208, v170, v171
	v_cvt_pk_fp8_f32 v209, v174, v175
	v_cvt_pk_fp8_f32 v210, v196, v197
	v_cvt_pk_fp8_f32 v211, v200, v201
	v_cvt_pk_fp8_f32 v208, v172, v173 op_sel:[0,0,1]
	v_cvt_pk_fp8_f32 v209, v176, v177 op_sel:[0,0,1]
	v_cvt_pk_fp8_f32 v210, v198, v199 op_sel:[0,0,1]
	v_cvt_pk_fp8_f32 v211, v202, v203 op_sel:[0,0,1]
	s_nop 0
	global_store_dwordx4 v12, v[208:211], s[14:15]
	s_waitcnt vmcnt(32)
	v_mul_f32_e32 v100, 0x43000000, v100
	v_mul_f32_e32 v101, 0x43000000, v101
	v_mul_f32_e32 v102, 0x43000000, v102
	v_mul_f32_e32 v103, 0x43000000, v103
	ds_write_b128 v4, v[100:103]
	v_mul_f32_e32 v104, 0x43000000, v104
	v_mul_f32_e32 v105, 0x43000000, v105
	v_mul_f32_e32 v106, 0x43000000, v106
	v_mul_f32_e32 v107, 0x43000000, v107
	ds_write_b128 v4, v[104:107] offset:1024
	v_mul_f32_e32 v108, 0x43000000, v108
	v_mul_f32_e32 v109, 0x43000000, v109
	v_mul_f32_e32 v110, 0x43000000, v110
	v_mul_f32_e32 v111, 0x43000000, v111
	ds_write_b128 v4, v[108:111] offset:2048
	v_mul_f32_e32 v112, 0x43000000, v112
	v_mul_f32_e32 v113, 0x43000000, v113
	v_mul_f32_e32 v114, 0x43000000, v114
	v_mul_f32_e32 v115, 0x43000000, v115
	ds_write_b128 v4, v[112:115] offset:3072
	v_mul_f32_e32 v116, 0x43000000, v116
	v_mul_f32_e32 v117, 0x43000000, v117
	v_mul_f32_e32 v118, 0x43000000, v118
	v_mul_f32_e32 v119, 0x43000000, v119
	ds_write_b128 v4, v[116:119] offset:4096
	v_mul_f32_e32 v120, 0x43000000, v120
	v_mul_f32_e32 v121, 0x43000000, v121
	v_mul_f32_e32 v122, 0x43000000, v122
	v_mul_f32_e32 v123, 0x43000000, v123
	ds_write_b128 v4, v[120:123] offset:5120
	v_mul_f32_e32 v124, 0x43000000, v124
	v_mul_f32_e32 v125, 0x43000000, v125
	v_mul_f32_e32 v126, 0x43000000, v126
	v_mul_f32_e32 v127, 0x43000000, v127
	ds_write_b128 v4, v[124:127] offset:6144
	v_mul_f32_e32 v128, 0x43000000, v128
	v_mul_f32_e32 v129, 0x43000000, v129
	v_mul_f32_e32 v130, 0x43000000, v130
	v_mul_f32_e32 v131, 0x43000000, v131
	ds_write_b128 v4, v[128:131] offset:7168
	s_waitcnt lgkmcnt(0)
	s_barrier
; #define GAS __attribute__((address_space(1)))
; #define LAS __attribute__((address_space(3)))
; #define LDS_WAIT() asm volatile("s_waitcnt lgkmcnt(0)" ::: "memory")
; __device__ __forceinline__ unsigned pk4_fp8(float a, float b, float c, float d) {
;     a = fminf(fmaxf(a, -448.f), 448.f); b = fminf(fmaxf(b, -448.f), 448.f); c = fminf(fmaxf(c, -448.f), 448.f); d = fminf(fmaxf(d, -448.f), 448.f);
;     int w = __builtin_amdgcn_cvt_pk_fp8_f32(a, b, 0, false); w = __builtin_amdgcn_cvt_pk_fp8_f32(c, d, w, true); return (unsigned)w; }
;     const int pr = item >> 1, kb = 2 * (pr / nblk) + (item & 1), nb = pr % nblk, k0 = 64 * kb, n0 = 32 * nb;
;     const int nr = n0 + (lane & 31); const int sc = MAP == 1 ? src_col_in(nr) : nr;
;     float v[32];
; #pragma unroll
;     for (int i = 0; i < 32; ++i) v[i] = sc >= 0 ? W[(size_t)(k0 + 2 * i + (lane >> 5)) * Nsrc + sc] : 0.f;
; #pragma unroll
;     for (int i = 0; i < 32; ++i) { const int k = k0 + 2 * i + (lane >> 5); float x = v[i] * wscale; if (KS) x *= (k < ksplit ? ksA[k] : ksB[k - ksplit]); scr[(2 * i + (lane >> 5)) * 33 + (lane & 31)] = x; }
;     LDS_WAIT(); asm volatile("" ::: "memory");
;     const int c = lane & 7;
; #pragma unroll
;     for (int j = 0; j < 4; ++j) { const int n = (lane >> 3) + 8 * j; const LAS float* s = scr + (8 * c) * 33 + n;
;         const unsigned long long o = (unsigned long long)pg8::pk4_fp8(s[0 * 33], s[1 * 33], s[2 * 33], s[3 * 33]) | ((unsigned long long)pg8::pk4_fp8(s[4 * 33], s[5 * 33], s[6 * 33], s[7 * 33]) << 32);
;         *(GAS unsigned long long*)(WT + (size_t)(n0 + n) * K + k0 + 8 * c) = o; }
;     LDS_WAIT(); asm volatile("" ::: "memory");
	s_add_i32 s17, s16, 1344
	s_min_u32 s17, s17, 0xfff
	s_lshr_b32 s18, s17, 5
	s_add_i32 s18, s18, 0
	s_and_b32 s19, s17, 31
	s_lshl_b32 s18, s18, 21
	s_lshl_b32 s19, s19, 9
	s_add_u32 s18, s18, s19
	s_add_u32 s12, s2, s18
	s_addc_u32 s13, s3, 0
	global_load_dwordx4 v[100:103], v10, s[12:13]
	s_add_u32 s12, s12, 0x8000
	s_addc_u32 s13, s13, 0
	global_load_dwordx4 v[104:107], v10, s[12:13]
	s_add_u32 s12, s12, 0x8000
	s_addc_u32 s13, s13, 0
	global_load_dwordx4 v[108:111], v10, s[12:13]
	s_add_u32 s12, s12, 0x8000
	s_addc_u32 s13, s13, 0
	global_load_dwordx4 v[112:115], v10, s[12:13]
	s_add_u32 s12, s12, 0x8000
	s_addc_u32 s13, s13, 0
	global_load_dwordx4 v[116:119], v10, s[12:13]
	s_add_u32 s12, s12, 0x8000
	s_addc_u32 s13, s13, 0
	global_load_dwordx4 v[120:123], v10, s[12:13]
	s_add_u32 s12, s12, 0x8000
	s_addc_u32 s13, s13, 0
	global_load_dwordx4 v[124:127], v10, s[12:13]
	s_add_u32 s12, s12, 0x8000
	s_addc_u32 s13, s13, 0
	global_load_dwordx4 v[128:131], v10, s[12:13]
	s_add_i32 s17, s16, 960
	s_min_u32 s17, s17, 0xfff
	s_lshr_b32 s18, s17, 5
	s_add_i32 s18, s18, 0
	s_and_b32 s19, s17, 31
	s_lshl_b32 s19, s19, 21
	s_lshl_b32 s18, s18, 7
	s_add_u32 s18, s18, s19
	s_add_u32 s14, s4, s18
	s_addc_u32 s15, s5, 0
	ds_read_b32 v170, v6
	ds_read_b32 v171, v6 offset:512
	ds_read_b32 v172, v6 offset:1024
	ds_read_b32 v173, v6 offset:1536
	ds_read_b32 v174, v6 offset:2048
	ds_read_b32 v175, v6 offset:2560
	ds_read_b32 v176, v6 offset:3072
	ds_read_b32 v177, v6 offset:3584
	ds_read_b32 v196, v6 offset:4096
	ds_read_b32 v197, v6 offset:4608
	ds_read_b32 v198, v6 offset:5120
	ds_read_b32 v199, v6 offset:5632
	ds_read_b32 v200, v6 offset:6144
	ds_read_b32 v201, v6 offset:6656
	ds_read_b32 v202, v6 offset:7168
	ds_read_b32 v203, v6 offset:7680
	s_waitcnt lgkmcnt(0)
	v_max_f32_e32 v170, v170, v170
	v_max_f32_e32 v171, v171, v171
	v_max_f32_e32 v172, v172, v172
	v_max_f32_e32 v173, v173, v173
	v_max_f32_e32 v174, v174, v174
	v_max_f32_e32 v175, v175, v175
	v_max_f32_e32 v176, v176, v176
	v_max_f32_e32 v177, v177, v177
	v_max_f32_e32 v196, v196, v196
	v_max_f32_e32 v197, v197, v197
	v_max_f32_e32 v198, v198, v198
	v_max_f32_e32 v199, v199, v199
	v_max_f32_e32 v200, v200, v200
	v_max_f32_e32 v201, v201, v201
	v_max_f32_e32 v202, v202, v202
	v_max_f32_e32 v203, v203, v203
	v_med3_f32 v170, v170, s20, v13
	v_med3_f32 v171, v171, s20, v13
	v_med3_f32 v172, v172, s20, v13
	v_med3_f32 v173, v173, s20, v13
	v_med3_f32 v174, v174, s20, v13
	v_med3_f32 v175, v175, s20, v13
	v_med3_f32 v176, v176, s20, v13
	v_med3_f32 v177, v177, s20, v13
	v_med3_f32 v196, v196, s20, v13
	v_med3_f32 v197, v197, s20, v13
	v_med3_f32 v198, v198, s20, v13
	v_med3_f32 v199, v199, s20, v13
	v_med3_f32 v200, v200, s20, v13
	v_med3_f32 v201, v201, s20, v13
	v_med3_f32 v202, v202, s20, v13
	v_med3_f32 v203, v203, s20, v13
	v_mov_b32_e32 v208, 0
	v_mov_b32_e32 v209, 0
	v_mov_b32_e32 v210, 0
	v_mov_b32_e32 v211, 0
	v_cvt_pk_fp8_f32 v208, v170, v171
	v_cvt_pk_fp8_f32 v209, v174, v175
	v_cvt_pk_fp8_f32 v210, v196, v197
	v_cvt_pk_fp8_f32 v211, v200, v201
	v_cvt_pk_fp8_f32 v208, v172, v173 op_sel:[0,0,1]
	v_cvt_pk_fp8_f32 v209, v176, v177 op_sel:[0,0,1]
	v_cvt_pk_fp8_f32 v210, v198, v199 op_sel:[0,0,1]
	v_cvt_pk_fp8_f32 v211, v202, v203 op_sel:[0,0,1]
	s_nop 0
	global_store_dwordx4 v11, v[208:211], s[14:15]
	ds_read_b32 v170, v8
	ds_read_b32 v171, v8 offset:512
	ds_read_b32 v172, v8 offset:1024
	ds_read_b32 v173, v8 offset:1536
	ds_read_b32 v174, v8 offset:2048
	ds_read_b32 v175, v8 offset:2560
	ds_read_b32 v176, v8 offset:3072
	ds_read_b32 v177, v8 offset:3584
	ds_read_b32 v196, v8 offset:4096
	ds_read_b32 v197, v8 offset:4608
	ds_read_b32 v198, v8 offset:5120
	ds_read_b32 v199, v8 offset:5632
	ds_read_b32 v200, v8 offset:6144
	ds_read_b32 v201, v8 offset:6656
	ds_read_b32 v202, v8 offset:7168
	ds_read_b32 v203, v8 offset:7680
	s_waitcnt lgkmcnt(0)
	v_max_f32_e32 v170, v170, v170
	v_max_f32_e32 v171, v171, v171
	v_max_f32_e32 v172, v172, v172
	v_max_f32_e32 v173, v173, v173
	v_max_f32_e32 v174, v174, v174
	v_max_f32_e32 v175, v175, v175
	v_max_f32_e32 v176, v176, v176
	v_max_f32_e32 v177, v177, v177
	v_max_f32_e32 v196, v196, v196
	v_max_f32_e32 v197, v197, v197
	v_max_f32_e32 v198, v198, v198
	v_max_f32_e32 v199, v199, v199
	v_max_f32_e32 v200, v200, v200
	v_max_f32_e32 v201, v201, v201
	v_max_f32_e32 v202, v202, v202
	v_max_f32_e32 v203, v203, v203
	v_med3_f32 v170, v170, s20, v13
	v_med3_f32 v171, v171, s20, v13
	v_med3_f32 v172, v172, s20, v13
	v_med3_f32 v173, v173, s20, v13
	v_med3_f32 v174, v174, s20, v13
	v_med3_f32 v175, v175, s20, v13
	v_med3_f32 v176, v176, s20, v13
	v_med3_f32 v177, v177, s20, v13
	v_med3_f32 v196, v196, s20, v13
	v_med3_f32 v197, v197, s20, v13
	v_med3_f32 v198, v198, s20, v13
	v_med3_f32 v199, v199, s20, v13
	v_med3_f32 v200, v200, s20, v13
	v_med3_f32 v201, v201, s20, v13
	v_med3_f32 v202, v202, s20, v13
	v_med3_f32 v203, v203, s20, v13
	v_mov_b32_e32 v208, 0
	v_mov_b32_e32 v209, 0
	v_mov_b32_e32 v210, 0
	v_mov_b32_e32 v211, 0
	v_cvt_pk_fp8_f32 v208, v170, v171
	v_cvt_pk_fp8_f32 v209, v174, v175
	v_cvt_pk_fp8_f32 v210, v196, v197
	v_cvt_pk_fp8_f32 v211, v200, v201
	v_cvt_pk_fp8_f32 v208, v172, v173 op_sel:[0,0,1]
	v_cvt_pk_fp8_f32 v209, v176, v177 op_sel:[0,0,1]
	v_cvt_pk_fp8_f32 v210, v198, v199 op_sel:[0,0,1]
	v_cvt_pk_fp8_f32 v211, v202, v203 op_sel:[0,0,1]
	s_nop 0
	global_store_dwordx4 v12, v[208:211], s[14:15]
	s_waitcnt vmcnt(32)
	v_mul_f32_e32 v132, 0x43000000, v132
	v_mul_f32_e32 v133, 0x43000000, v133
	v_mul_f32_e32 v134, 0x43000000, v134
	v_mul_f32_e32 v135, 0x43000000, v135
	ds_write_b128 v5, v[132:135]
	v_mul_f32_e32 v136, 0x43000000, v136
	v_mul_f32_e32 v137, 0x43000000, v137
	v_mul_f32_e32 v138, 0x43000000, v138
	v_mul_f32_e32 v139, 0x43000000, v139
	ds_write_b128 v5, v[136:139] offset:1024
	v_mul_f32_e32 v140, 0x43000000, v140
	v_mul_f32_e32 v141, 0x43000000, v141
	v_mul_f32_e32 v142, 0x43000000, v142
	v_mul_f32_e32 v143, 0x43000000, v143
	ds_write_b128 v5, v[140:143] offset:2048
	v_mul_f32_e32 v144, 0x43000000, v144
	v_mul_f32_e32 v145, 0x43000000, v145
	v_mul_f32_e32 v146, 0x43000000, v146
	v_mul_f32_e32 v147, 0x43000000, v147
	ds_write_b128 v5, v[144:147] offset:3072
	v_mul_f32_e32 v148, 0x43000000, v148
	v_mul_f32_e32 v149, 0x43000000, v149
	v_mul_f32_e32 v150, 0x43000000, v150
	v_mul_f32_e32 v151, 0x43000000, v151
	ds_write_b128 v5, v[148:151] offset:4096
	v_mul_f32_e32 v152, 0x43000000, v152
	v_mul_f32_e32 v153, 0x43000000, v153
	v_mul_f32_e32 v154, 0x43000000, v154
	v_mul_f32_e32 v155, 0x43000000, v155
	ds_write_b128 v5, v[152:155] offset:5120
	v_mul_f32_e32 v156, 0x43000000, v156
	v_mul_f32_e32 v157, 0x43000000, v157
	v_mul_f32_e32 v158, 0x43000000, v158
	v_mul_f32_e32 v159, 0x43000000, v159
	ds_write_b128 v5, v[156:159] offset:6144
	v_mul_f32_e32 v160, 0x43000000, v160
	v_mul_f32_e32 v161, 0x43000000, v161
	v_mul_f32_e32 v162, 0x43000000, v162
	v_mul_f32_e32 v163, 0x43000000, v163
	ds_write_b128 v5, v[160:163] offset:7168
	s_waitcnt lgkmcnt(0)
	s_barrier
; #define GAS __attribute__((address_space(1)))
; #define LAS __attribute__((address_space(3)))
; #define LDS_WAIT() asm volatile("s_waitcnt lgkmcnt(0)" ::: "memory")
; __device__ __forceinline__ unsigned pk4_fp8(float a, float b, float c, float d) {
;     a = fminf(fmaxf(a, -448.f), 448.f); b = fminf(fmaxf(b, -448.f), 448.f); c = fminf(fmaxf(c, -448.f), 448.f); d = fminf(fmaxf(d, -448.f), 448.f);
;     int w = __builtin_amdgcn_cvt_pk_fp8_f32(a, b, 0, false); w = __builtin_amdgcn_cvt_pk_fp8_f32(c, d, w, true); return (unsigned)w; }
;     const int pr = item >> 1, kb = 2 * (pr / nblk) + (item & 1), nb = pr % nblk, k0 = 64 * kb, n0 = 32 * nb;
;     const int nr = n0 + (lane & 31); const int sc = MAP == 1 ? src_col_in(nr) : nr;
;     float v[32];
; #pragma unroll
;     for (int i = 0; i < 32; ++i) v[i] = sc >= 0 ? W[(size_t)(k0 + 2 * i + (lane >> 5)) * Nsrc + sc] : 0.f;
; #pragma unroll
;     for (int i = 0; i < 32; ++i) { const int k = k0 + 2 * i + (lane >> 5); float x = v[i] * wscale; if (KS) x *= (k < ksplit ? ksA[k] : ksB[k - ksplit]); scr[(2 * i + (lane >> 5)) * 33 + (lane & 31)] = x; }
;     LDS_WAIT(); asm volatile("" ::: "memory");
;     const int c = lane & 7;
; #pragma unroll
;     for (int j = 0; j < 4; ++j) { const int n = (lane >> 3) + 8 * j; const LAS float* s = scr + (8 * c) * 33 + n;
;         const unsigned long long o = (unsigned long long)pg8::pk4_fp8(s[0 * 33], s[1 * 33], s[2 * 33], s[3 * 33]) | ((unsigned long long)pg8::pk4_fp8(s[4 * 33], s[5 * 33], s[6 * 33], s[7 * 33]) << 32);
;         *(GAS unsigned long long*)(WT + (size_t)(n0 + n) * K + k0 + 8 * c) = o; }
;     LDS_WAIT(); asm volatile("" ::: "memory");
	s_add_i32 s17, s16, 1440
	s_min_u32 s17, s17, 0xfff
	s_lshr_b32 s18, s17, 5
	s_add_i32 s18, s18, 0
	s_and_b32 s19, s17, 31
	s_lshl_b32 s18, s18, 21
	s_lshl_b32 s19, s19, 9
	s_add_u32 s18, s18, s19
	s_add_u32 s12, s2, s18
	s_addc_u32 s13, s3, 0
	global_load_dwordx4 v[132:135], v10, s[12:13]
	s_add_u32 s12, s12, 0x8000
	s_addc_u32 s13, s13, 0
	global_load_dwordx4 v[136:139], v10, s[12:13]
	s_add_u32 s12, s12, 0x8000
	s_addc_u32 s13, s13, 0
	global_load_dwordx4 v[140:143], v10, s[12:13]
	s_add_u32 s12, s12, 0x8000
	s_addc_u32 s13, s13, 0
	global_load_dwordx4 v[144:147], v10, s[12:13]
	s_add_u32 s12, s12, 0x8000
	s_addc_u32 s13, s13, 0
	global_load_dwordx4 v[148:151], v10, s[12:13]
	s_add_u32 s12, s12, 0x8000
	s_addc_u32 s13, s13, 0
	global_load_dwordx4 v[152:155], v10, s[12:13]
	s_add_u32 s12, s12, 0x8000
	s_addc_u32 s13, s13, 0
	global_load_dwordx4 v[156:159], v10, s[12:13]
	s_add_u32 s12, s12, 0x8000
	s_addc_u32 s13, s13, 0
	global_load_dwordx4 v[160:163], v10, s[12:13]
	s_add_i32 s17, s16, 1056
	s_min_u32 s17, s17, 0xfff
	s_lshr_b32 s18, s17, 5
	s_add_i32 s18, s18, 0
	s_and_b32 s19, s17, 31
	s_lshl_b32 s19, s19, 21
	s_lshl_b32 s18, s18, 7
	s_add_u32 s18, s18, s19
	s_add_u32 s14, s4, s18
	s_addc_u32 s15, s5, 0
	ds_read_b32 v170, v7
	ds_read_b32 v171, v7 offset:512
	ds_read_b32 v172, v7 offset:1024
	ds_read_b32 v173, v7 offset:1536
	ds_read_b32 v174, v7 offset:2048
	ds_read_b32 v175, v7 offset:2560
	ds_read_b32 v176, v7 offset:3072
	ds_read_b32 v177, v7 offset:3584
	ds_read_b32 v196, v7 offset:4096
	ds_read_b32 v197, v7 offset:4608
	ds_read_b32 v198, v7 offset:5120
	ds_read_b32 v199, v7 offset:5632
	ds_read_b32 v200, v7 offset:6144
	ds_read_b32 v201, v7 offset:6656
	ds_read_b32 v202, v7 offset:7168
	ds_read_b32 v203, v7 offset:7680
	s_waitcnt lgkmcnt(0)
	v_max_f32_e32 v170, v170, v170
	v_max_f32_e32 v171, v171, v171
	v_max_f32_e32 v172, v172, v172
	v_max_f32_e32 v173, v173, v173
	v_max_f32_e32 v174, v174, v174
	v_max_f32_e32 v175, v175, v175
	v_max_f32_e32 v176, v176, v176
	v_max_f32_e32 v177, v177, v177
	v_max_f32_e32 v196, v196, v196
	v_max_f32_e32 v197, v197, v197
	v_max_f32_e32 v198, v198, v198
	v_max_f32_e32 v199, v199, v199
	v_max_f32_e32 v200, v200, v200
	v_max_f32_e32 v201, v201, v201
	v_max_f32_e32 v202, v202, v202
	v_max_f32_e32 v203, v203, v203
	v_med3_f32 v170, v170, s20, v13
	v_med3_f32 v171, v171, s20, v13
	v_med3_f32 v172, v172, s20, v13
	v_med3_f32 v173, v173, s20, v13
	v_med3_f32 v174, v174, s20, v13
	v_med3_f32 v175, v175, s20, v13
	v_med3_f32 v176, v176, s20, v13
	v_med3_f32 v177, v177, s20, v13
	v_med3_f32 v196, v196, s20, v13
	v_med3_f32 v197, v197, s20, v13
	v_med3_f32 v198, v198, s20, v13
	v_med3_f32 v199, v199, s20, v13
	v_med3_f32 v200, v200, s20, v13
	v_med3_f32 v201, v201, s20, v13
	v_med3_f32 v202, v202, s20, v13
	v_med3_f32 v203, v203, s20, v13
	v_mov_b32_e32 v208, 0
	v_mov_b32_e32 v209, 0
	v_mov_b32_e32 v210, 0
	v_mov_b32_e32 v211, 0
	v_cvt_pk_fp8_f32 v208, v170, v171
	v_cvt_pk_fp8_f32 v209, v174, v175
	v_cvt_pk_fp8_f32 v210, v196, v197
	v_cvt_pk_fp8_f32 v211, v200, v201
	v_cvt_pk_fp8_f32 v208, v172, v173 op_sel:[0,0,1]
	v_cvt_pk_fp8_f32 v209, v176, v177 op_sel:[0,0,1]
	v_cvt_pk_fp8_f32 v210, v198, v199 op_sel:[0,0,1]
	v_cvt_pk_fp8_f32 v211, v202, v203 op_sel:[0,0,1]
	s_nop 0
	global_store_dwordx4 v11, v[208:211], s[14:15]
	ds_read_b32 v170, v9
	ds_read_b32 v171, v9 offset:512
	ds_read_b32 v172, v9 offset:1024
	ds_read_b32 v173, v9 offset:1536
	ds_read_b32 v174, v9 offset:2048
	ds_read_b32 v175, v9 offset:2560
	ds_read_b32 v176, v9 offset:3072
	ds_read_b32 v177, v9 offset:3584
	ds_read_b32 v196, v9 offset:4096
	ds_read_b32 v197, v9 offset:4608
	ds_read_b32 v198, v9 offset:5120
	ds_read_b32 v199, v9 offset:5632
	ds_read_b32 v200, v9 offset:6144
	ds_read_b32 v201, v9 offset:6656
	ds_read_b32 v202, v9 offset:7168
	ds_read_b32 v203, v9 offset:7680
	s_waitcnt lgkmcnt(0)
	v_max_f32_e32 v170, v170, v170
	v_max_f32_e32 v171, v171, v171
	v_max_f32_e32 v172, v172, v172
	v_max_f32_e32 v173, v173, v173
	v_max_f32_e32 v174, v174, v174
	v_max_f32_e32 v175, v175, v175
	v_max_f32_e32 v176, v176, v176
	v_max_f32_e32 v177, v177, v177
	v_max_f32_e32 v196, v196, v196
	v_max_f32_e32 v197, v197, v197
	v_max_f32_e32 v198, v198, v198
	v_max_f32_e32 v199, v199, v199
	v_max_f32_e32 v200, v200, v200
	v_max_f32_e32 v201, v201, v201
	v_max_f32_e32 v202, v202, v202
	v_max_f32_e32 v203, v203, v203
	v_med3_f32 v170, v170, s20, v13
	v_med3_f32 v171, v171, s20, v13
	v_med3_f32 v172, v172, s20, v13
	v_med3_f32 v173, v173, s20, v13
	v_med3_f32 v174, v174, s20, v13
	v_med3_f32 v175, v175, s20, v13
	v_med3_f32 v176, v176, s20, v13
	v_med3_f32 v177, v177, s20, v13
	v_med3_f32 v196, v196, s20, v13
	v_med3_f32 v197, v197, s20, v13
	v_med3_f32 v198, v198, s20, v13
	v_med3_f32 v199, v199, s20, v13
	v_med3_f32 v200, v200, s20, v13
	v_med3_f32 v201, v201, s20, v13
	v_med3_f32 v202, v202, s20, v13
	v_med3_f32 v203, v203, s20, v13
	v_mov_b32_e32 v208, 0
	v_mov_b32_e32 v209, 0
	v_mov_b32_e32 v210, 0
	v_mov_b32_e32 v211, 0
	v_cvt_pk_fp8_f32 v208, v170, v171
	v_cvt_pk_fp8_f32 v209, v174, v175
	v_cvt_pk_fp8_f32 v210, v196, v197
	v_cvt_pk_fp8_f32 v211, v200, v201
	v_cvt_pk_fp8_f32 v208, v172, v173 op_sel:[0,0,1]
	v_cvt_pk_fp8_f32 v209, v176, v177 op_sel:[0,0,1]
	v_cvt_pk_fp8_f32 v210, v198, v199 op_sel:[0,0,1]
	v_cvt_pk_fp8_f32 v211, v202, v203 op_sel:[0,0,1]
	s_nop 0
	global_store_dwordx4 v12, v[208:211], s[14:15]
	s_waitcnt vmcnt(32)
	v_mul_f32_e32 v36, 0x43000000, v36
	v_mul_f32_e32 v37, 0x43000000, v37
	v_mul_f32_e32 v38, 0x43000000, v38
	v_mul_f32_e32 v39, 0x43000000, v39
	ds_write_b128 v4, v[36:39]
	v_mul_f32_e32 v40, 0x43000000, v40
	v_mul_f32_e32 v41, 0x43000000, v41
	v_mul_f32_e32 v42, 0x43000000, v42
	v_mul_f32_e32 v43, 0x43000000, v43
	ds_write_b128 v4, v[40:43] offset:1024
	v_mul_f32_e32 v44, 0x43000000, v44
	v_mul_f32_e32 v45, 0x43000000, v45
	v_mul_f32_e32 v46, 0x43000000, v46
	v_mul_f32_e32 v47, 0x43000000, v47
	ds_write_b128 v4, v[44:47] offset:2048
	v_mul_f32_e32 v48, 0x43000000, v48
	v_mul_f32_e32 v49, 0x43000000, v49
	v_mul_f32_e32 v50, 0x43000000, v50
	v_mul_f32_e32 v51, 0x43000000, v51
	ds_write_b128 v4, v[48:51] offset:3072
	v_mul_f32_e32 v52, 0x43000000, v52
	v_mul_f32_e32 v53, 0x43000000, v53
	v_mul_f32_e32 v54, 0x43000000, v54
	v_mul_f32_e32 v55, 0x43000000, v55
	ds_write_b128 v4, v[52:55] offset:4096
	v_mul_f32_e32 v56, 0x43000000, v56
	v_mul_f32_e32 v57, 0x43000000, v57
	v_mul_f32_e32 v58, 0x43000000, v58
	v_mul_f32_e32 v59, 0x43000000, v59
	ds_write_b128 v4, v[56:59] offset:5120
	v_mul_f32_e32 v60, 0x43000000, v60
	v_mul_f32_e32 v61, 0x43000000, v61
	v_mul_f32_e32 v62, 0x43000000, v62
	v_mul_f32_e32 v63, 0x43000000, v63
	ds_write_b128 v4, v[60:63] offset:6144
	v_mul_f32_e32 v64, 0x43000000, v64
	v_mul_f32_e32 v65, 0x43000000, v65
	v_mul_f32_e32 v66, 0x43000000, v66
	v_mul_f32_e32 v67, 0x43000000, v67
	ds_write_b128 v4, v[64:67] offset:7168
	s_waitcnt lgkmcnt(0)
	s_barrier
; #define GAS __attribute__((address_space(1)))
; #define LAS __attribute__((address_space(3)))
; #define LDS_WAIT() asm volatile("s_waitcnt lgkmcnt(0)" ::: "memory")
; __device__ __forceinline__ unsigned pk4_fp8(float a, float b, float c, float d) {
;     a = fminf(fmaxf(a, -448.f), 448.f); b = fminf(fmaxf(b, -448.f), 448.f); c = fminf(fmaxf(c, -448.f), 448.f); d = fminf(fmaxf(d, -448.f), 448.f);
;     int w = __builtin_amdgcn_cvt_pk_fp8_f32(a, b, 0, false); w = __builtin_amdgcn_cvt_pk_fp8_f32(c, d, w, true); return (unsigned)w; }
;     const int pr = item >> 1, kb = 2 * (pr / nblk) + (item & 1), nb = pr % nblk, k0 = 64 * kb, n0 = 32 * nb;
;     const int nr = n0 + (lane & 31); const int sc = MAP == 1 ? src_col_in(nr) : nr;
;     float v[32];
; #pragma unroll
;     for (int i = 0; i < 32; ++i) v[i] = sc >= 0 ? W[(size_t)(k0 + 2 * i + (lane >> 5)) * Nsrc + sc] : 0.f;
; #pragma unroll
;     for (int i = 0; i < 32; ++i) { const int k = k0 + 2 * i + (lane >> 5); float x = v[i] * wscale; if (KS) x *= (k < ksplit ? ksA[k] : ksB[k - ksplit]); scr[(2 * i + (lane >> 5)) * 33 + (lane & 31)] = x; }
;     LDS_WAIT(); asm volatile("" ::: "memory");
;     const int c = lane & 7;
; #pragma unroll
;     for (int j = 0; j < 4; ++j) { const int n = (lane >> 3) + 8 * j; const LAS float* s = scr + (8 * c) * 33 + n;
;         const unsigned long long o = (unsigned long long)pg8::pk4_fp8(s[0 * 33], s[1 * 33], s[2 * 33], s[3 * 33]) | ((unsigned long long)pg8::pk4_fp8(s[4 * 33], s[5 * 33], s[6 * 33], s[7 * 33]) << 32);
;         *(GAS unsigned long long*)(WT + (size_t)(n0 + n) * K + k0 + 8 * c) = o; }
;     LDS_WAIT(); asm volatile("" ::: "memory");
	s_add_i32 s17, s16, 1536
	s_min_u32 s17, s17, 0xfff
	s_lshr_b32 s18, s17, 5
	s_add_i32 s18, s18, 0
	s_and_b32 s19, s17, 31
	s_lshl_b32 s18, s18, 21
	s_lshl_b32 s19, s19, 9
	s_add_u32 s18, s18, s19
	s_add_u32 s12, s2, s18
	s_addc_u32 s13, s3, 0
	global_load_dwordx4 v[36:39], v10, s[12:13]
	s_add_u32 s12, s12, 0x8000
	s_addc_u32 s13, s13, 0
	global_load_dwordx4 v[40:43], v10, s[12:13]
	s_add_u32 s12, s12, 0x8000
	s_addc_u32 s13, s13, 0
	global_load_dwordx4 v[44:47], v10, s[12:13]
	s_add_u32 s12, s12, 0x8000
	s_addc_u32 s13, s13, 0
	global_load_dwordx4 v[48:51], v10, s[12:13]
	s_add_u32 s12, s12, 0x8000
	s_addc_u32 s13, s13, 0
	global_load_dwordx4 v[52:55], v10, s[12:13]
	s_add_u32 s12, s12, 0x8000
	s_addc_u32 s13, s13, 0
	global_load_dwordx4 v[56:59], v10, s[12:13]
	s_add_u32 s12, s12, 0x8000
	s_addc_u32 s13, s13, 0
	global_load_dwordx4 v[60:63], v10, s[12:13]
	s_add_u32 s12, s12, 0x8000
	s_addc_u32 s13, s13, 0
	global_load_dwordx4 v[64:67], v10, s[12:13]
	s_add_i32 s17, s16, 1152
	s_min_u32 s17, s17, 0xfff
	s_lshr_b32 s18, s17, 5
	s_add_i32 s18, s18, 0
	s_and_b32 s19, s17, 31
	s_lshl_b32 s19, s19, 21
	s_lshl_b32 s18, s18, 7
	s_add_u32 s18, s18, s19
	s_add_u32 s14, s4, s18
	s_addc_u32 s15, s5, 0
	ds_read_b32 v170, v6
	ds_read_b32 v171, v6 offset:512
	ds_read_b32 v172, v6 offset:1024
	ds_read_b32 v173, v6 offset:1536
	ds_read_b32 v174, v6 offset:2048
	ds_read_b32 v175, v6 offset:2560
	ds_read_b32 v176, v6 offset:3072
	ds_read_b32 v177, v6 offset:3584
	ds_read_b32 v196, v6 offset:4096
	ds_read_b32 v197, v6 offset:4608
	ds_read_b32 v198, v6 offset:5120
	ds_read_b32 v199, v6 offset:5632
	ds_read_b32 v200, v6 offset:6144
	ds_read_b32 v201, v6 offset:6656
	ds_read_b32 v202, v6 offset:7168
	ds_read_b32 v203, v6 offset:7680
	s_waitcnt lgkmcnt(0)
	v_max_f32_e32 v170, v170, v170
	v_max_f32_e32 v171, v171, v171
	v_max_f32_e32 v172, v172, v172
	v_max_f32_e32 v173, v173, v173
	v_max_f32_e32 v174, v174, v174
	v_max_f32_e32 v175, v175, v175
	v_max_f32_e32 v176, v176, v176
	v_max_f32_e32 v177, v177, v177
	v_max_f32_e32 v196, v196, v196
	v_max_f32_e32 v197, v197, v197
	v_max_f32_e32 v198, v198, v198
	v_max_f32_e32 v199, v199, v199
	v_max_f32_e32 v200, v200, v200
	v_max_f32_e32 v201, v201, v201
	v_max_f32_e32 v202, v202, v202
	v_max_f32_e32 v203, v203, v203
	v_med3_f32 v170, v170, s20, v13
	v_med3_f32 v171, v171, s20, v13
	v_med3_f32 v172, v172, s20, v13
	v_med3_f32 v173, v173, s20, v13
	v_med3_f32 v174, v174, s20, v13
	v_med3_f32 v175, v175, s20, v13
	v_med3_f32 v176, v176, s20, v13
	v_med3_f32 v177, v177, s20, v13
	v_med3_f32 v196, v196, s20, v13
	v_med3_f32 v197, v197, s20, v13
	v_med3_f32 v198, v198, s20, v13
	v_med3_f32 v199, v199, s20, v13
	v_med3_f32 v200, v200, s20, v13
	v_med3_f32 v201, v201, s20, v13
	v_med3_f32 v202, v202, s20, v13
	v_med3_f32 v203, v203, s20, v13
	v_mov_b32_e32 v208, 0
	v_mov_b32_e32 v209, 0
	v_mov_b32_e32 v210, 0
	v_mov_b32_e32 v211, 0
	v_cvt_pk_fp8_f32 v208, v170, v171
	v_cvt_pk_fp8_f32 v209, v174, v175
	v_cvt_pk_fp8_f32 v210, v196, v197
	v_cvt_pk_fp8_f32 v211, v200, v201
	v_cvt_pk_fp8_f32 v208, v172, v173 op_sel:[0,0,1]
	v_cvt_pk_fp8_f32 v209, v176, v177 op_sel:[0,0,1]
	v_cvt_pk_fp8_f32 v210, v198, v199 op_sel:[0,0,1]
	v_cvt_pk_fp8_f32 v211, v202, v203 op_sel:[0,0,1]
	s_nop 0
	global_store_dwordx4 v11, v[208:211], s[14:15]
	ds_read_b32 v170, v8
	ds_read_b32 v171, v8 offset:512
	ds_read_b32 v172, v8 offset:1024
	ds_read_b32 v173, v8 offset:1536
	ds_read_b32 v174, v8 offset:2048
	ds_read_b32 v175, v8 offset:2560
	ds_read_b32 v176, v8 offset:3072
	ds_read_b32 v177, v8 offset:3584
	ds_read_b32 v196, v8 offset:4096
	ds_read_b32 v197, v8 offset:4608
	ds_read_b32 v198, v8 offset:5120
	ds_read_b32 v199, v8 offset:5632
	ds_read_b32 v200, v8 offset:6144
	ds_read_b32 v201, v8 offset:6656
	ds_read_b32 v202, v8 offset:7168
	ds_read_b32 v203, v8 offset:7680
	s_waitcnt lgkmcnt(0)
	v_max_f32_e32 v170, v170, v170
	v_max_f32_e32 v171, v171, v171
	v_max_f32_e32 v172, v172, v172
	v_max_f32_e32 v173, v173, v173
	v_max_f32_e32 v174, v174, v174
	v_max_f32_e32 v175, v175, v175
	v_max_f32_e32 v176, v176, v176
	v_max_f32_e32 v177, v177, v177
	v_max_f32_e32 v196, v196, v196
	v_max_f32_e32 v197, v197, v197
	v_max_f32_e32 v198, v198, v198
	v_max_f32_e32 v199, v199, v199
	v_max_f32_e32 v200, v200, v200
	v_max_f32_e32 v201, v201, v201
	v_max_f32_e32 v202, v202, v202
	v_max_f32_e32 v203, v203, v203
	v_med3_f32 v170, v170, s20, v13
	v_med3_f32 v171, v171, s20, v13
	v_med3_f32 v172, v172, s20, v13
	v_med3_f32 v173, v173, s20, v13
	v_med3_f32 v174, v174, s20, v13
	v_med3_f32 v175, v175, s20, v13
	v_med3_f32 v176, v176, s20, v13
	v_med3_f32 v177, v177, s20, v13
	v_med3_f32 v196, v196, s20, v13
	v_med3_f32 v197, v197, s20, v13
	v_med3_f32 v198, v198, s20, v13
	v_med3_f32 v199, v199, s20, v13
	v_med3_f32 v200, v200, s20, v13
	v_med3_f32 v201, v201, s20, v13
	v_med3_f32 v202, v202, s20, v13
	v_med3_f32 v203, v203, s20, v13
	v_mov_b32_e32 v208, 0
	v_mov_b32_e32 v209, 0
	v_mov_b32_e32 v210, 0
	v_mov_b32_e32 v211, 0
	v_cvt_pk_fp8_f32 v208, v170, v171
	v_cvt_pk_fp8_f32 v209, v174, v175
	v_cvt_pk_fp8_f32 v210, v196, v197
	v_cvt_pk_fp8_f32 v211, v200, v201
	v_cvt_pk_fp8_f32 v208, v172, v173 op_sel:[0,0,1]
	v_cvt_pk_fp8_f32 v209, v176, v177 op_sel:[0,0,1]
	v_cvt_pk_fp8_f32 v210, v198, v199 op_sel:[0,0,1]
	v_cvt_pk_fp8_f32 v211, v202, v203 op_sel:[0,0,1]
	s_nop 0
	global_store_dwordx4 v12, v[208:211], s[14:15]
	s_waitcnt vmcnt(32)
	v_mul_f32_e32 v68, 0x43000000, v68
	v_mul_f32_e32 v69, 0x43000000, v69
	v_mul_f32_e32 v70, 0x43000000, v70
	v_mul_f32_e32 v71, 0x43000000, v71
	ds_write_b128 v5, v[68:71]
	v_mul_f32_e32 v72, 0x43000000, v72
	v_mul_f32_e32 v73, 0x43000000, v73
	v_mul_f32_e32 v74, 0x43000000, v74
	v_mul_f32_e32 v75, 0x43000000, v75
	ds_write_b128 v5, v[72:75] offset:1024
	v_mul_f32_e32 v76, 0x43000000, v76
	v_mul_f32_e32 v77, 0x43000000, v77
	v_mul_f32_e32 v78, 0x43000000, v78
	v_mul_f32_e32 v79, 0x43000000, v79
	ds_write_b128 v5, v[76:79] offset:2048
	v_mul_f32_e32 v80, 0x43000000, v80
	v_mul_f32_e32 v81, 0x43000000, v81
	v_mul_f32_e32 v82, 0x43000000, v82
	v_mul_f32_e32 v83, 0x43000000, v83
	ds_write_b128 v5, v[80:83] offset:3072
	v_mul_f32_e32 v84, 0x43000000, v84
	v_mul_f32_e32 v85, 0x43000000, v85
	v_mul_f32_e32 v86, 0x43000000, v86
	v_mul_f32_e32 v87, 0x43000000, v87
	ds_write_b128 v5, v[84:87] offset:4096
	v_mul_f32_e32 v88, 0x43000000, v88
	v_mul_f32_e32 v89, 0x43000000, v89
	v_mul_f32_e32 v90, 0x43000000, v90
	v_mul_f32_e32 v91, 0x43000000, v91
	ds_write_b128 v5, v[88:91] offset:5120
	v_mul_f32_e32 v92, 0x43000000, v92
	v_mul_f32_e32 v93, 0x43000000, v93
	v_mul_f32_e32 v94, 0x43000000, v94
	v_mul_f32_e32 v95, 0x43000000, v95
	ds_write_b128 v5, v[92:95] offset:6144
	v_mul_f32_e32 v96, 0x43000000, v96
	v_mul_f32_e32 v97, 0x43000000, v97
	v_mul_f32_e32 v98, 0x43000000, v98
	v_mul_f32_e32 v99, 0x43000000, v99
	ds_write_b128 v5, v[96:99] offset:7168
	s_waitcnt lgkmcnt(0)
	s_barrier
; #define GAS __attribute__((address_space(1)))
; #define LAS __attribute__((address_space(3)))
; #define LDS_WAIT() asm volatile("s_waitcnt lgkmcnt(0)" ::: "memory")
; __device__ __forceinline__ unsigned pk4_fp8(float a, float b, float c, float d) {
;     a = fminf(fmaxf(a, -448.f), 448.f); b = fminf(fmaxf(b, -448.f), 448.f); c = fminf(fmaxf(c, -448.f), 448.f); d = fminf(fmaxf(d, -448.f), 448.f);
;     int w = __builtin_amdgcn_cvt_pk_fp8_f32(a, b, 0, false); w = __builtin_amdgcn_cvt_pk_fp8_f32(c, d, w, true); return (unsigned)w; }
;     const int pr = item >> 1, kb = 2 * (pr / nblk) + (item & 1), nb = pr % nblk, k0 = 64 * kb, n0 = 32 * nb;
;     const int nr = n0 + (lane & 31); const int sc = MAP == 1 ? src_col_in(nr) : nr;
;     float v[32];
; #pragma unroll
;     for (int i = 0; i < 32; ++i) v[i] = sc >= 0 ? W[(size_t)(k0 + 2 * i + (lane >> 5)) * Nsrc + sc] : 0.f;
; #pragma unroll
;     for (int i = 0; i < 32; ++i) { const int k = k0 + 2 * i + (lane >> 5); float x = v[i] * wscale; if (KS) x *= (k < ksplit ? ksA[k] : ksB[k - ksplit]); scr[(2 * i + (lane >> 5)) * 33 + (lane & 31)] = x; }
;     LDS_WAIT(); asm volatile("" ::: "memory");
;     const int c = lane & 7;
; #pragma unroll
;     for (int j = 0; j < 4; ++j) { const int n = (lane >> 3) + 8 * j; const LAS float* s = scr + (8 * c) * 33 + n;
;         const unsigned long long o = (unsigned long long)pg8::pk4_fp8(s[0 * 33], s[1 * 33], s[2 * 33], s[3 * 33]) | ((unsigned long long)pg8::pk4_fp8(s[4 * 33], s[5 * 33], s[6 * 33], s[7 * 33]) << 32);
;         *(GAS unsigned long long*)(WT + (size_t)(n0 + n) * K + k0 + 8 * c) = o; }
;     LDS_WAIT(); asm volatile("" ::: "memory");
	s_add_i32 s17, s16, 1632
	s_min_u32 s17, s17, 0xfff
	s_lshr_b32 s18, s17, 5
	s_add_i32 s18, s18, 0
	s_and_b32 s19, s17, 31
	s_lshl_b32 s18, s18, 21
	s_lshl_b32 s19, s19, 9
	s_add_u32 s18, s18, s19
	s_add_u32 s12, s2, s18
	s_addc_u32 s13, s3, 0
	global_load_dwordx4 v[68:71], v10, s[12:13]
	s_add_u32 s12, s12, 0x8000
	s_addc_u32 s13, s13, 0
	global_load_dwordx4 v[72:75], v10, s[12:13]
	s_add_u32 s12, s12, 0x8000
	s_addc_u32 s13, s13, 0
	global_load_dwordx4 v[76:79], v10, s[12:13]
	s_add_u32 s12, s12, 0x8000
	s_addc_u32 s13, s13, 0
	global_load_dwordx4 v[80:83], v10, s[12:13]
	s_add_u32 s12, s12, 0x8000
	s_addc_u32 s13, s13, 0
	global_load_dwordx4 v[84:87], v10, s[12:13]
	s_add_u32 s12, s12, 0x8000
	s_addc_u32 s13, s13, 0
	global_load_dwordx4 v[88:91], v10, s[12:13]
	s_add_u32 s12, s12, 0x8000
	s_addc_u32 s13, s13, 0
	global_load_dwordx4 v[92:95], v10, s[12:13]
	s_add_u32 s12, s12, 0x8000
	s_addc_u32 s13, s13, 0
	global_load_dwordx4 v[96:99], v10, s[12:13]
	s_add_i32 s17, s16, 1248
	s_min_u32 s17, s17, 0xfff
	s_lshr_b32 s18, s17, 5
	s_add_i32 s18, s18, 0
	s_and_b32 s19, s17, 31
	s_lshl_b32 s19, s19, 21
	s_lshl_b32 s18, s18, 7
	s_add_u32 s18, s18, s19
	s_add_u32 s14, s4, s18
	s_addc_u32 s15, s5, 0
	ds_read_b32 v170, v7
	ds_read_b32 v171, v7 offset:512
	ds_read_b32 v172, v7 offset:1024
	ds_read_b32 v173, v7 offset:1536
	ds_read_b32 v174, v7 offset:2048
	ds_read_b32 v175, v7 offset:2560
	ds_read_b32 v176, v7 offset:3072
	ds_read_b32 v177, v7 offset:3584
	ds_read_b32 v196, v7 offset:4096
	ds_read_b32 v197, v7 offset:4608
	ds_read_b32 v198, v7 offset:5120
	ds_read_b32 v199, v7 offset:5632
	ds_read_b32 v200, v7 offset:6144
	ds_read_b32 v201, v7 offset:6656
	ds_read_b32 v202, v7 offset:7168
	ds_read_b32 v203, v7 offset:7680
	s_waitcnt lgkmcnt(0)
	v_max_f32_e32 v170, v170, v170
	v_max_f32_e32 v171, v171, v171
	v_max_f32_e32 v172, v172, v172
	v_max_f32_e32 v173, v173, v173
	v_max_f32_e32 v174, v174, v174
	v_max_f32_e32 v175, v175, v175
	v_max_f32_e32 v176, v176, v176
	v_max_f32_e32 v177, v177, v177
	v_max_f32_e32 v196, v196, v196
	v_max_f32_e32 v197, v197, v197
	v_max_f32_e32 v198, v198, v198
	v_max_f32_e32 v199, v199, v199
	v_max_f32_e32 v200, v200, v200
	v_max_f32_e32 v201, v201, v201
	v_max_f32_e32 v202, v202, v202
	v_max_f32_e32 v203, v203, v203
	v_med3_f32 v170, v170, s20, v13
	v_med3_f32 v171, v171, s20, v13
	v_med3_f32 v172, v172, s20, v13
	v_med3_f32 v173, v173, s20, v13
	v_med3_f32 v174, v174, s20, v13
	v_med3_f32 v175, v175, s20, v13
	v_med3_f32 v176, v176, s20, v13
	v_med3_f32 v177, v177, s20, v13
	v_med3_f32 v196, v196, s20, v13
	v_med3_f32 v197, v197, s20, v13
	v_med3_f32 v198, v198, s20, v13
	v_med3_f32 v199, v199, s20, v13
	v_med3_f32 v200, v200, s20, v13
	v_med3_f32 v201, v201, s20, v13
	v_med3_f32 v202, v202, s20, v13
	v_med3_f32 v203, v203, s20, v13
	v_mov_b32_e32 v208, 0
	v_mov_b32_e32 v209, 0
	v_mov_b32_e32 v210, 0
	v_mov_b32_e32 v211, 0
	v_cvt_pk_fp8_f32 v208, v170, v171
	v_cvt_pk_fp8_f32 v209, v174, v175
	v_cvt_pk_fp8_f32 v210, v196, v197
	v_cvt_pk_fp8_f32 v211, v200, v201
	v_cvt_pk_fp8_f32 v208, v172, v173 op_sel:[0,0,1]
	v_cvt_pk_fp8_f32 v209, v176, v177 op_sel:[0,0,1]
	v_cvt_pk_fp8_f32 v210, v198, v199 op_sel:[0,0,1]
	v_cvt_pk_fp8_f32 v211, v202, v203 op_sel:[0,0,1]
	s_nop 0
	global_store_dwordx4 v11, v[208:211], s[14:15]
	ds_read_b32 v170, v9
	ds_read_b32 v171, v9 offset:512
	ds_read_b32 v172, v9 offset:1024
	ds_read_b32 v173, v9 offset:1536
	ds_read_b32 v174, v9 offset:2048
	ds_read_b32 v175, v9 offset:2560
	ds_read_b32 v176, v9 offset:3072
	ds_read_b32 v177, v9 offset:3584
	ds_read_b32 v196, v9 offset:4096
	ds_read_b32 v197, v9 offset:4608
	ds_read_b32 v198, v9 offset:5120
	ds_read_b32 v199, v9 offset:5632
	ds_read_b32 v200, v9 offset:6144
	ds_read_b32 v201, v9 offset:6656
	ds_read_b32 v202, v9 offset:7168
	ds_read_b32 v203, v9 offset:7680
	s_waitcnt lgkmcnt(0)
	v_max_f32_e32 v170, v170, v170
	v_max_f32_e32 v171, v171, v171
	v_max_f32_e32 v172, v172, v172
	v_max_f32_e32 v173, v173, v173
	v_max_f32_e32 v174, v174, v174
	v_max_f32_e32 v175, v175, v175
	v_max_f32_e32 v176, v176, v176
	v_max_f32_e32 v177, v177, v177
	v_max_f32_e32 v196, v196, v196
	v_max_f32_e32 v197, v197, v197
	v_max_f32_e32 v198, v198, v198
	v_max_f32_e32 v199, v199, v199
	v_max_f32_e32 v200, v200, v200
	v_max_f32_e32 v201, v201, v201
	v_max_f32_e32 v202, v202, v202
	v_max_f32_e32 v203, v203, v203
	v_med3_f32 v170, v170, s20, v13
	v_med3_f32 v171, v171, s20, v13
	v_med3_f32 v172, v172, s20, v13
	v_med3_f32 v173, v173, s20, v13
	v_med3_f32 v174, v174, s20, v13
	v_med3_f32 v175, v175, s20, v13
	v_med3_f32 v176, v176, s20, v13
	v_med3_f32 v177, v177, s20, v13
	v_med3_f32 v196, v196, s20, v13
	v_med3_f32 v197, v197, s20, v13
	v_med3_f32 v198, v198, s20, v13
	v_med3_f32 v199, v199, s20, v13
	v_med3_f32 v200, v200, s20, v13
	v_med3_f32 v201, v201, s20, v13
	v_med3_f32 v202, v202, s20, v13
	v_med3_f32 v203, v203, s20, v13
	v_mov_b32_e32 v208, 0
	v_mov_b32_e32 v209, 0
	v_mov_b32_e32 v210, 0
	v_mov_b32_e32 v211, 0
	v_cvt_pk_fp8_f32 v208, v170, v171
	v_cvt_pk_fp8_f32 v209, v174, v175
	v_cvt_pk_fp8_f32 v210, v196, v197
	v_cvt_pk_fp8_f32 v211, v200, v201
	v_cvt_pk_fp8_f32 v208, v172, v173 op_sel:[0,0,1]
	v_cvt_pk_fp8_f32 v209, v176, v177 op_sel:[0,0,1]
	v_cvt_pk_fp8_f32 v210, v198, v199 op_sel:[0,0,1]
	v_cvt_pk_fp8_f32 v211, v202, v203 op_sel:[0,0,1]
	s_nop 0
	global_store_dwordx4 v12, v[208:211], s[14:15]
	s_waitcnt vmcnt(32)
	v_mul_f32_e32 v100, 0x43000000, v100
	v_mul_f32_e32 v101, 0x43000000, v101
	v_mul_f32_e32 v102, 0x43000000, v102
	v_mul_f32_e32 v103, 0x43000000, v103
	ds_write_b128 v4, v[100:103]
	v_mul_f32_e32 v104, 0x43000000, v104
	v_mul_f32_e32 v105, 0x43000000, v105
	v_mul_f32_e32 v106, 0x43000000, v106
	v_mul_f32_e32 v107, 0x43000000, v107
	ds_write_b128 v4, v[104:107] offset:1024
	v_mul_f32_e32 v108, 0x43000000, v108
	v_mul_f32_e32 v109, 0x43000000, v109
	v_mul_f32_e32 v110, 0x43000000, v110
	v_mul_f32_e32 v111, 0x43000000, v111
	ds_write_b128 v4, v[108:111] offset:2048
	v_mul_f32_e32 v112, 0x43000000, v112
	v_mul_f32_e32 v113, 0x43000000, v113
	v_mul_f32_e32 v114, 0x43000000, v114
	v_mul_f32_e32 v115, 0x43000000, v115
	ds_write_b128 v4, v[112:115] offset:3072
	v_mul_f32_e32 v116, 0x43000000, v116
	v_mul_f32_e32 v117, 0x43000000, v117
	v_mul_f32_e32 v118, 0x43000000, v118
	v_mul_f32_e32 v119, 0x43000000, v119
	ds_write_b128 v4, v[116:119] offset:4096
	v_mul_f32_e32 v120, 0x43000000, v120
	v_mul_f32_e32 v121, 0x43000000, v121
	v_mul_f32_e32 v122, 0x43000000, v122
	v_mul_f32_e32 v123, 0x43000000, v123
	ds_write_b128 v4, v[120:123] offset:5120
	v_mul_f32_e32 v124, 0x43000000, v124
	v_mul_f32_e32 v125, 0x43000000, v125
	v_mul_f32_e32 v126, 0x43000000, v126
	v_mul_f32_e32 v127, 0x43000000, v127
	ds_write_b128 v4, v[124:127] offset:6144
	v_mul_f32_e32 v128, 0x43000000, v128
	v_mul_f32_e32 v129, 0x43000000, v129
	v_mul_f32_e32 v130, 0x43000000, v130
	v_mul_f32_e32 v131, 0x43000000, v131
	ds_write_b128 v4, v[128:131] offset:7168
	s_waitcnt lgkmcnt(0)
	s_barrier
; #define GAS __attribute__((address_space(1)))
; #define LAS __attribute__((address_space(3)))
; #define LDS_WAIT() asm volatile("s_waitcnt lgkmcnt(0)" ::: "memory")
; __device__ __forceinline__ unsigned pk4_fp8(float a, float b, float c, float d) {
;     a = fminf(fmaxf(a, -448.f), 448.f); b = fminf(fmaxf(b, -448.f), 448.f); c = fminf(fmaxf(c, -448.f), 448.f); d = fminf(fmaxf(d, -448.f), 448.f);
;     int w = __builtin_amdgcn_cvt_pk_fp8_f32(a, b, 0, false); w = __builtin_amdgcn_cvt_pk_fp8_f32(c, d, w, true); return (unsigned)w; }
;     const int pr = item >> 1, kb = 2 * (pr / nblk) + (item & 1), nb = pr % nblk, k0 = 64 * kb, n0 = 32 * nb;
;     const int nr = n0 + (lane & 31); const int sc = MAP == 1 ? src_col_in(nr) : nr;
;     float v[32];
; #pragma unroll
;     for (int i = 0; i < 32; ++i) v[i] = sc >= 0 ? W[(size_t)(k0 + 2 * i + (lane >> 5)) * Nsrc + sc] : 0.f;
; #pragma unroll
;     for (int i = 0; i < 32; ++i) { const int k = k0 + 2 * i + (lane >> 5); float x = v[i] * wscale; if (KS) x *= (k < ksplit ? ksA[k] : ksB[k - ksplit]); scr[(2 * i + (lane >> 5)) * 33 + (lane & 31)] = x; }
;     LDS_WAIT(); asm volatile("" ::: "memory");
;     const int c = lane & 7;
; #pragma unroll
;     for (int j = 0; j < 4; ++j) { const int n = (lane >> 3) + 8 * j; const LAS float* s = scr + (8 * c) * 33 + n;
;         const unsigned long long o = (unsigned long long)pg8::pk4_fp8(s[0 * 33], s[1 * 33], s[2 * 33], s[3 * 33]) | ((unsigned long long)pg8::pk4_fp8(s[4 * 33], s[5 * 33], s[6 * 33], s[7 * 33]) << 32);
;         *(GAS unsigned long long*)(WT + (size_t)(n0 + n) * K + k0 + 8 * c) = o; }
;     LDS_WAIT(); asm volatile("" ::: "memory");
	s_add_i32 s17, s16, 1728
	s_min_u32 s17, s17, 0xfff
	s_lshr_b32 s18, s17, 5
	s_add_i32 s18, s18, 0
	s_and_b32 s19, s17, 31
	s_lshl_b32 s18, s18, 21
	s_lshl_b32 s19, s19, 9
	s_add_u32 s18, s18, s19
	s_add_u32 s12, s2, s18
	s_addc_u32 s13, s3, 0
	global_load_dwordx4 v[100:103], v10, s[12:13]
	s_add_u32 s12, s12, 0x8000
	s_addc_u32 s13, s13, 0
	global_load_dwordx4 v[104:107], v10, s[12:13]
	s_add_u32 s12, s12, 0x8000
	s_addc_u32 s13, s13, 0
	global_load_dwordx4 v[108:111], v10, s[12:13]
	s_add_u32 s12, s12, 0x8000
	s_addc_u32 s13, s13, 0
	global_load_dwordx4 v[112:115], v10, s[12:13]
	s_add_u32 s12, s12, 0x8000
	s_addc_u32 s13, s13, 0
	global_load_dwordx4 v[116:119], v10, s[12:13]
	s_add_u32 s12, s12, 0x8000
	s_addc_u32 s13, s13, 0
	global_load_dwordx4 v[120:123], v10, s[12:13]
	s_add_u32 s12, s12, 0x8000
	s_addc_u32 s13, s13, 0
	global_load_dwordx4 v[124:127], v10, s[12:13]
	s_add_u32 s12, s12, 0x8000
	s_addc_u32 s13, s13, 0
	global_load_dwordx4 v[128:131], v10, s[12:13]
	s_add_i32 s17, s16, 1344
	s_min_u32 s17, s17, 0xfff
	s_lshr_b32 s18, s17, 5
	s_add_i32 s18, s18, 0
	s_and_b32 s19, s17, 31
	s_lshl_b32 s19, s19, 21
	s_lshl_b32 s18, s18, 7
	s_add_u32 s18, s18, s19
	s_add_u32 s14, s4, s18
	s_addc_u32 s15, s5, 0
	ds_read_b32 v170, v6
	ds_read_b32 v171, v6 offset:512
	ds_read_b32 v172, v6 offset:1024
	ds_read_b32 v173, v6 offset:1536
	ds_read_b32 v174, v6 offset:2048
	ds_read_b32 v175, v6 offset:2560
	ds_read_b32 v176, v6 offset:3072
	ds_read_b32 v177, v6 offset:3584
	ds_read_b32 v196, v6 offset:4096
	ds_read_b32 v197, v6 offset:4608
	ds_read_b32 v198, v6 offset:5120
	ds_read_b32 v199, v6 offset:5632
	ds_read_b32 v200, v6 offset:6144
	ds_read_b32 v201, v6 offset:6656
	ds_read_b32 v202, v6 offset:7168
	ds_read_b32 v203, v6 offset:7680
	s_waitcnt lgkmcnt(0)
	v_max_f32_e32 v170, v170, v170
	v_max_f32_e32 v171, v171, v171
	v_max_f32_e32 v172, v172, v172
	v_max_f32_e32 v173, v173, v173
	v_max_f32_e32 v174, v174, v174
	v_max_f32_e32 v175, v175, v175
	v_max_f32_e32 v176, v176, v176
	v_max_f32_e32 v177, v177, v177
	v_max_f32_e32 v196, v196, v196
	v_max_f32_e32 v197, v197, v197
	v_max_f32_e32 v198, v198, v198
	v_max_f32_e32 v199, v199, v199
	v_max_f32_e32 v200, v200, v200
	v_max_f32_e32 v201, v201, v201
	v_max_f32_e32 v202, v202, v202
	v_max_f32_e32 v203, v203, v203
	v_med3_f32 v170, v170, s20, v13
	v_med3_f32 v171, v171, s20, v13
	v_med3_f32 v172, v172, s20, v13
	v_med3_f32 v173, v173, s20, v13
	v_med3_f32 v174, v174, s20, v13
	v_med3_f32 v175, v175, s20, v13
	v_med3_f32 v176, v176, s20, v13
	v_med3_f32 v177, v177, s20, v13
	v_med3_f32 v196, v196, s20, v13
	v_med3_f32 v197, v197, s20, v13
	v_med3_f32 v198, v198, s20, v13
	v_med3_f32 v199, v199, s20, v13
	v_med3_f32 v200, v200, s20, v13
	v_med3_f32 v201, v201, s20, v13
	v_med3_f32 v202, v202, s20, v13
	v_med3_f32 v203, v203, s20, v13
	v_mov_b32_e32 v208, 0
	v_mov_b32_e32 v209, 0
	v_mov_b32_e32 v210, 0
	v_mov_b32_e32 v211, 0
	v_cvt_pk_fp8_f32 v208, v170, v171
	v_cvt_pk_fp8_f32 v209, v174, v175
	v_cvt_pk_fp8_f32 v210, v196, v197
	v_cvt_pk_fp8_f32 v211, v200, v201
	v_cvt_pk_fp8_f32 v208, v172, v173 op_sel:[0,0,1]
	v_cvt_pk_fp8_f32 v209, v176, v177 op_sel:[0,0,1]
	v_cvt_pk_fp8_f32 v210, v198, v199 op_sel:[0,0,1]
	v_cvt_pk_fp8_f32 v211, v202, v203 op_sel:[0,0,1]
	s_nop 0
	global_store_dwordx4 v11, v[208:211], s[14:15]
	ds_read_b32 v170, v8
	ds_read_b32 v171, v8 offset:512
	ds_read_b32 v172, v8 offset:1024
	ds_read_b32 v173, v8 offset:1536
	ds_read_b32 v174, v8 offset:2048
	ds_read_b32 v175, v8 offset:2560
	ds_read_b32 v176, v8 offset:3072
	ds_read_b32 v177, v8 offset:3584
	ds_read_b32 v196, v8 offset:4096
	ds_read_b32 v197, v8 offset:4608
	ds_read_b32 v198, v8 offset:5120
	ds_read_b32 v199, v8 offset:5632
	ds_read_b32 v200, v8 offset:6144
	ds_read_b32 v201, v8 offset:6656
	ds_read_b32 v202, v8 offset:7168
	ds_read_b32 v203, v8 offset:7680
	s_waitcnt lgkmcnt(0)
	v_max_f32_e32 v170, v170, v170
	v_max_f32_e32 v171, v171, v171
	v_max_f32_e32 v172, v172, v172
	v_max_f32_e32 v173, v173, v173
	v_max_f32_e32 v174, v174, v174
	v_max_f32_e32 v175, v175, v175
	v_max_f32_e32 v176, v176, v176
	v_max_f32_e32 v177, v177, v177
	v_max_f32_e32 v196, v196, v196
	v_max_f32_e32 v197, v197, v197
	v_max_f32_e32 v198, v198, v198
	v_max_f32_e32 v199, v199, v199
	v_max_f32_e32 v200, v200, v200
	v_max_f32_e32 v201, v201, v201
	v_max_f32_e32 v202, v202, v202
	v_max_f32_e32 v203, v203, v203
	v_med3_f32 v170, v170, s20, v13
	v_med3_f32 v171, v171, s20, v13
	v_med3_f32 v172, v172, s20, v13
	v_med3_f32 v173, v173, s20, v13
	v_med3_f32 v174, v174, s20, v13
	v_med3_f32 v175, v175, s20, v13
	v_med3_f32 v176, v176, s20, v13
	v_med3_f32 v177, v177, s20, v13
	v_med3_f32 v196, v196, s20, v13
	v_med3_f32 v197, v197, s20, v13
	v_med3_f32 v198, v198, s20, v13
	v_med3_f32 v199, v199, s20, v13
	v_med3_f32 v200, v200, s20, v13
	v_med3_f32 v201, v201, s20, v13
	v_med3_f32 v202, v202, s20, v13
	v_med3_f32 v203, v203, s20, v13
	v_mov_b32_e32 v208, 0
	v_mov_b32_e32 v209, 0
	v_mov_b32_e32 v210, 0
	v_mov_b32_e32 v211, 0
	v_cvt_pk_fp8_f32 v208, v170, v171
	v_cvt_pk_fp8_f32 v209, v174, v175
	v_cvt_pk_fp8_f32 v210, v196, v197
	v_cvt_pk_fp8_f32 v211, v200, v201
	v_cvt_pk_fp8_f32 v208, v172, v173 op_sel:[0,0,1]
	v_cvt_pk_fp8_f32 v209, v176, v177 op_sel:[0,0,1]
	v_cvt_pk_fp8_f32 v210, v198, v199 op_sel:[0,0,1]
	v_cvt_pk_fp8_f32 v211, v202, v203 op_sel:[0,0,1]
	s_nop 0
	global_store_dwordx4 v12, v[208:211], s[14:15]
	s_waitcnt vmcnt(32)
	v_mul_f32_e32 v132, 0x43000000, v132
	v_mul_f32_e32 v133, 0x43000000, v133
	v_mul_f32_e32 v134, 0x43000000, v134
	v_mul_f32_e32 v135, 0x43000000, v135
	ds_write_b128 v5, v[132:135]
	v_mul_f32_e32 v136, 0x43000000, v136
	v_mul_f32_e32 v137, 0x43000000, v137
	v_mul_f32_e32 v138, 0x43000000, v138
	v_mul_f32_e32 v139, 0x43000000, v139
	ds_write_b128 v5, v[136:139] offset:1024
	v_mul_f32_e32 v140, 0x43000000, v140
	v_mul_f32_e32 v141, 0x43000000, v141
	v_mul_f32_e32 v142, 0x43000000, v142
	v_mul_f32_e32 v143, 0x43000000, v143
	ds_write_b128 v5, v[140:143] offset:2048
	v_mul_f32_e32 v144, 0x43000000, v144
	v_mul_f32_e32 v145, 0x43000000, v145
	v_mul_f32_e32 v146, 0x43000000, v146
	v_mul_f32_e32 v147, 0x43000000, v147
	ds_write_b128 v5, v[144:147] offset:3072
	v_mul_f32_e32 v148, 0x43000000, v148
	v_mul_f32_e32 v149, 0x43000000, v149
	v_mul_f32_e32 v150, 0x43000000, v150
	v_mul_f32_e32 v151, 0x43000000, v151
	ds_write_b128 v5, v[148:151] offset:4096
	v_mul_f32_e32 v152, 0x43000000, v152
	v_mul_f32_e32 v153, 0x43000000, v153
	v_mul_f32_e32 v154, 0x43000000, v154
	v_mul_f32_e32 v155, 0x43000000, v155
	ds_write_b128 v5, v[152:155] offset:5120
	v_mul_f32_e32 v156, 0x43000000, v156
	v_mul_f32_e32 v157, 0x43000000, v157
	v_mul_f32_e32 v158, 0x43000000, v158
	v_mul_f32_e32 v159, 0x43000000, v159
	ds_write_b128 v5, v[156:159] offset:6144
	v_mul_f32_e32 v160, 0x43000000, v160
	v_mul_f32_e32 v161, 0x43000000, v161
	v_mul_f32_e32 v162, 0x43000000, v162
	v_mul_f32_e32 v163, 0x43000000, v163
	ds_write_b128 v5, v[160:163] offset:7168
	s_waitcnt lgkmcnt(0)
	s_barrier
; #define GAS __attribute__((address_space(1)))
; #define LAS __attribute__((address_space(3)))
; #define LDS_WAIT() asm volatile("s_waitcnt lgkmcnt(0)" ::: "memory")
; __device__ __forceinline__ unsigned pk4_fp8(float a, float b, float c, float d) {
;     a = fminf(fmaxf(a, -448.f), 448.f); b = fminf(fmaxf(b, -448.f), 448.f); c = fminf(fmaxf(c, -448.f), 448.f); d = fminf(fmaxf(d, -448.f), 448.f);
;     int w = __builtin_amdgcn_cvt_pk_fp8_f32(a, b, 0, false); w = __builtin_amdgcn_cvt_pk_fp8_f32(c, d, w, true); return (unsigned)w; }
;     const int pr = item >> 1, kb = 2 * (pr / nblk) + (item & 1), nb = pr % nblk, k0 = 64 * kb, n0 = 32 * nb;
;     const int nr = n0 + (lane & 31); const int sc = MAP == 1 ? src_col_in(nr) : nr;
;     float v[32];
; #pragma unroll
;     for (int i = 0; i < 32; ++i) v[i] = sc >= 0 ? W[(size_t)(k0 + 2 * i + (lane >> 5)) * Nsrc + sc] : 0.f;
; #pragma unroll
;     for (int i = 0; i < 32; ++i) { const int k = k0 + 2 * i + (lane >> 5); float x = v[i] * wscale; if (KS) x *= (k < ksplit ? ksA[k] : ksB[k - ksplit]); scr[(2 * i + (lane >> 5)) * 33 + (lane & 31)] = x; }
;     LDS_WAIT(); asm volatile("" ::: "memory");
;     const int c = lane & 7;
; #pragma unroll
;     for (int j = 0; j < 4; ++j) { const int n = (lane >> 3) + 8 * j; const LAS float* s = scr + (8 * c) * 33 + n;
;         const unsigned long long o = (unsigned long long)pg8::pk4_fp8(s[0 * 33], s[1 * 33], s[2 * 33], s[3 * 33]) | ((unsigned long long)pg8::pk4_fp8(s[4 * 33], s[5 * 33], s[6 * 33], s[7 * 33]) << 32);
;         *(GAS unsigned long long*)(WT + (size_t)(n0 + n) * K + k0 + 8 * c) = o; }
;     LDS_WAIT(); asm volatile("" ::: "memory");
	s_add_i32 s17, s16, 1824
	s_min_u32 s17, s17, 0xfff
	s_lshr_b32 s18, s17, 5
	s_add_i32 s18, s18, 0
	s_and_b32 s19, s17, 31
	s_lshl_b32 s18, s18, 21
	s_lshl_b32 s19, s19, 9
	s_add_u32 s18, s18, s19
	s_add_u32 s12, s2, s18
	s_addc_u32 s13, s3, 0
	global_load_dwordx4 v[132:135], v10, s[12:13]
	s_add_u32 s12, s12, 0x8000
	s_addc_u32 s13, s13, 0
	global_load_dwordx4 v[136:139], v10, s[12:13]
	s_add_u32 s12, s12, 0x8000
	s_addc_u32 s13, s13, 0
	global_load_dwordx4 v[140:143], v10, s[12:13]
	s_add_u32 s12, s12, 0x8000
	s_addc_u32 s13, s13, 0
	global_load_dwordx4 v[144:147], v10, s[12:13]
	s_add_u32 s12, s12, 0x8000
	s_addc_u32 s13, s13, 0
	global_load_dwordx4 v[148:151], v10, s[12:13]
	s_add_u32 s12, s12, 0x8000
	s_addc_u32 s13, s13, 0
	global_load_dwordx4 v[152:155], v10, s[12:13]
	s_add_u32 s12, s12, 0x8000
	s_addc_u32 s13, s13, 0
	global_load_dwordx4 v[156:159], v10, s[12:13]
	s_add_u32 s12, s12, 0x8000
	s_addc_u32 s13, s13, 0
	global_load_dwordx4 v[160:163], v10, s[12:13]
	s_add_i32 s17, s16, 1440
	s_min_u32 s17, s17, 0xfff
	s_lshr_b32 s18, s17, 5
	s_add_i32 s18, s18, 0
	s_and_b32 s19, s17, 31
	s_lshl_b32 s19, s19, 21
	s_lshl_b32 s18, s18, 7
	s_add_u32 s18, s18, s19
	s_add_u32 s14, s4, s18
	s_addc_u32 s15, s5, 0
	ds_read_b32 v170, v7
	ds_read_b32 v171, v7 offset:512
	ds_read_b32 v172, v7 offset:1024
	ds_read_b32 v173, v7 offset:1536
	ds_read_b32 v174, v7 offset:2048
	ds_read_b32 v175, v7 offset:2560
	ds_read_b32 v176, v7 offset:3072
	ds_read_b32 v177, v7 offset:3584
	ds_read_b32 v196, v7 offset:4096
	ds_read_b32 v197, v7 offset:4608
	ds_read_b32 v198, v7 offset:5120
	ds_read_b32 v199, v7 offset:5632
	ds_read_b32 v200, v7 offset:6144
	ds_read_b32 v201, v7 offset:6656
	ds_read_b32 v202, v7 offset:7168
	ds_read_b32 v203, v7 offset:7680
	s_waitcnt lgkmcnt(0)
	v_max_f32_e32 v170, v170, v170
	v_max_f32_e32 v171, v171, v171
	v_max_f32_e32 v172, v172, v172
	v_max_f32_e32 v173, v173, v173
	v_max_f32_e32 v174, v174, v174
	v_max_f32_e32 v175, v175, v175
	v_max_f32_e32 v176, v176, v176
	v_max_f32_e32 v177, v177, v177
	v_max_f32_e32 v196, v196, v196
	v_max_f32_e32 v197, v197, v197
	v_max_f32_e32 v198, v198, v198
	v_max_f32_e32 v199, v199, v199
	v_max_f32_e32 v200, v200, v200
	v_max_f32_e32 v201, v201, v201
	v_max_f32_e32 v202, v202, v202
	v_max_f32_e32 v203, v203, v203
	v_med3_f32 v170, v170, s20, v13
	v_med3_f32 v171, v171, s20, v13
	v_med3_f32 v172, v172, s20, v13
	v_med3_f32 v173, v173, s20, v13
	v_med3_f32 v174, v174, s20, v13
	v_med3_f32 v175, v175, s20, v13
	v_med3_f32 v176, v176, s20, v13
	v_med3_f32 v177, v177, s20, v13
	v_med3_f32 v196, v196, s20, v13
	v_med3_f32 v197, v197, s20, v13
	v_med3_f32 v198, v198, s20, v13
	v_med3_f32 v199, v199, s20, v13
	v_med3_f32 v200, v200, s20, v13
	v_med3_f32 v201, v201, s20, v13
	v_med3_f32 v202, v202, s20, v13
	v_med3_f32 v203, v203, s20, v13
	v_mov_b32_e32 v208, 0
	v_mov_b32_e32 v209, 0
	v_mov_b32_e32 v210, 0
	v_mov_b32_e32 v211, 0
	v_cvt_pk_fp8_f32 v208, v170, v171
	v_cvt_pk_fp8_f32 v209, v174, v175
	v_cvt_pk_fp8_f32 v210, v196, v197
	v_cvt_pk_fp8_f32 v211, v200, v201
	v_cvt_pk_fp8_f32 v208, v172, v173 op_sel:[0,0,1]
	v_cvt_pk_fp8_f32 v209, v176, v177 op_sel:[0,0,1]
	v_cvt_pk_fp8_f32 v210, v198, v199 op_sel:[0,0,1]
	v_cvt_pk_fp8_f32 v211, v202, v203 op_sel:[0,0,1]
	s_nop 0
	global_store_dwordx4 v11, v[208:211], s[14:15]
	ds_read_b32 v170, v9
	ds_read_b32 v171, v9 offset:512
	ds_read_b32 v172, v9 offset:1024
	ds_read_b32 v173, v9 offset:1536
	ds_read_b32 v174, v9 offset:2048
	ds_read_b32 v175, v9 offset:2560
	ds_read_b32 v176, v9 offset:3072
	ds_read_b32 v177, v9 offset:3584
	ds_read_b32 v196, v9 offset:4096
	ds_read_b32 v197, v9 offset:4608
	ds_read_b32 v198, v9 offset:5120
	ds_read_b32 v199, v9 offset:5632
	ds_read_b32 v200, v9 offset:6144
	ds_read_b32 v201, v9 offset:6656
	ds_read_b32 v202, v9 offset:7168
	ds_read_b32 v203, v9 offset:7680
	s_waitcnt lgkmcnt(0)
	v_max_f32_e32 v170, v170, v170
	v_max_f32_e32 v171, v171, v171
	v_max_f32_e32 v172, v172, v172
	v_max_f32_e32 v173, v173, v173
	v_max_f32_e32 v174, v174, v174
	v_max_f32_e32 v175, v175, v175
	v_max_f32_e32 v176, v176, v176
	v_max_f32_e32 v177, v177, v177
	v_max_f32_e32 v196, v196, v196
	v_max_f32_e32 v197, v197, v197
	v_max_f32_e32 v198, v198, v198
	v_max_f32_e32 v199, v199, v199
	v_max_f32_e32 v200, v200, v200
	v_max_f32_e32 v201, v201, v201
	v_max_f32_e32 v202, v202, v202
	v_max_f32_e32 v203, v203, v203
	v_med3_f32 v170, v170, s20, v13
	v_med3_f32 v171, v171, s20, v13
	v_med3_f32 v172, v172, s20, v13
	v_med3_f32 v173, v173, s20, v13
	v_med3_f32 v174, v174, s20, v13
	v_med3_f32 v175, v175, s20, v13
	v_med3_f32 v176, v176, s20, v13
	v_med3_f32 v177, v177, s20, v13
	v_med3_f32 v196, v196, s20, v13
	v_med3_f32 v197, v197, s20, v13
	v_med3_f32 v198, v198, s20, v13
	v_med3_f32 v199, v199, s20, v13
	v_med3_f32 v200, v200, s20, v13
	v_med3_f32 v201, v201, s20, v13
	v_med3_f32 v202, v202, s20, v13
	v_med3_f32 v203, v203, s20, v13
	v_mov_b32_e32 v208, 0
	v_mov_b32_e32 v209, 0
	v_mov_b32_e32 v210, 0
	v_mov_b32_e32 v211, 0
	v_cvt_pk_fp8_f32 v208, v170, v171
	v_cvt_pk_fp8_f32 v209, v174, v175
	v_cvt_pk_fp8_f32 v210, v196, v197
	v_cvt_pk_fp8_f32 v211, v200, v201
	v_cvt_pk_fp8_f32 v208, v172, v173 op_sel:[0,0,1]
	v_cvt_pk_fp8_f32 v209, v176, v177 op_sel:[0,0,1]
	v_cvt_pk_fp8_f32 v210, v198, v199 op_sel:[0,0,1]
	v_cvt_pk_fp8_f32 v211, v202, v203 op_sel:[0,0,1]
	s_nop 0
	global_store_dwordx4 v12, v[208:211], s[14:15]
	s_waitcnt vmcnt(32)
	v_mul_f32_e32 v36, 0x43000000, v36
	v_mul_f32_e32 v37, 0x43000000, v37
	v_mul_f32_e32 v38, 0x43000000, v38
	v_mul_f32_e32 v39, 0x43000000, v39
	ds_write_b128 v4, v[36:39]
	v_mul_f32_e32 v40, 0x43000000, v40
	v_mul_f32_e32 v41, 0x43000000, v41
	v_mul_f32_e32 v42, 0x43000000, v42
	v_mul_f32_e32 v43, 0x43000000, v43
	ds_write_b128 v4, v[40:43] offset:1024
	v_mul_f32_e32 v44, 0x43000000, v44
	v_mul_f32_e32 v45, 0x43000000, v45
	v_mul_f32_e32 v46, 0x43000000, v46
	v_mul_f32_e32 v47, 0x43000000, v47
	ds_write_b128 v4, v[44:47] offset:2048
	v_mul_f32_e32 v48, 0x43000000, v48
	v_mul_f32_e32 v49, 0x43000000, v49
	v_mul_f32_e32 v50, 0x43000000, v50
	v_mul_f32_e32 v51, 0x43000000, v51
	ds_write_b128 v4, v[48:51] offset:3072
	v_mul_f32_e32 v52, 0x43000000, v52
	v_mul_f32_e32 v53, 0x43000000, v53
	v_mul_f32_e32 v54, 0x43000000, v54
	v_mul_f32_e32 v55, 0x43000000, v55
	ds_write_b128 v4, v[52:55] offset:4096
	v_mul_f32_e32 v56, 0x43000000, v56
	v_mul_f32_e32 v57, 0x43000000, v57
	v_mul_f32_e32 v58, 0x43000000, v58
	v_mul_f32_e32 v59, 0x43000000, v59
	ds_write_b128 v4, v[56:59] offset:5120
	v_mul_f32_e32 v60, 0x43000000, v60
	v_mul_f32_e32 v61, 0x43000000, v61
	v_mul_f32_e32 v62, 0x43000000, v62
	v_mul_f32_e32 v63, 0x43000000, v63
	ds_write_b128 v4, v[60:63] offset:6144
	v_mul_f32_e32 v64, 0x43000000, v64
	v_mul_f32_e32 v65, 0x43000000, v65
	v_mul_f32_e32 v66, 0x43000000, v66
	v_mul_f32_e32 v67, 0x43000000, v67
	ds_write_b128 v4, v[64:67] offset:7168
	s_waitcnt lgkmcnt(0)
	s_barrier
; #define GAS __attribute__((address_space(1)))
; #define LAS __attribute__((address_space(3)))
; #define LDS_WAIT() asm volatile("s_waitcnt lgkmcnt(0)" ::: "memory")
; __device__ __forceinline__ unsigned pk4_fp8(float a, float b, float c, float d) {
;     a = fminf(fmaxf(a, -448.f), 448.f); b = fminf(fmaxf(b, -448.f), 448.f); c = fminf(fmaxf(c, -448.f), 448.f); d = fminf(fmaxf(d, -448.f), 448.f);
;     int w = __builtin_amdgcn_cvt_pk_fp8_f32(a, b, 0, false); w = __builtin_amdgcn_cvt_pk_fp8_f32(c, d, w, true); return (unsigned)w; }
;     const int pr = item >> 1, kb = 2 * (pr / nblk) + (item & 1), nb = pr % nblk, k0 = 64 * kb, n0 = 32 * nb;
;     const int nr = n0 + (lane & 31); const int sc = MAP == 1 ? src_col_in(nr) : nr;
;     float v[32];
; #pragma unroll
;     for (int i = 0; i < 32; ++i) v[i] = sc >= 0 ? W[(size_t)(k0 + 2 * i + (lane >> 5)) * Nsrc + sc] : 0.f;
; #pragma unroll
;     for (int i = 0; i < 32; ++i) { const int k = k0 + 2 * i + (lane >> 5); float x = v[i] * wscale; if (KS) x *= (k < ksplit ? ksA[k] : ksB[k - ksplit]); scr[(2 * i + (lane >> 5)) * 33 + (lane & 31)] = x; }
;     LDS_WAIT(); asm volatile("" ::: "memory");
;     const int c = lane & 7;
; #pragma unroll
;     for (int j = 0; j < 4; ++j) { const int n = (lane >> 3) + 8 * j; const LAS float* s = scr + (8 * c) * 33 + n;
;         const unsigned long long o = (unsigned long long)pg8::pk4_fp8(s[0 * 33], s[1 * 33], s[2 * 33], s[3 * 33]) | ((unsigned long long)pg8::pk4_fp8(s[4 * 33], s[5 * 33], s[6 * 33], s[7 * 33]) << 32);
;         *(GAS unsigned long long*)(WT + (size_t)(n0 + n) * K + k0 + 8 * c) = o; }
;     LDS_WAIT(); asm volatile("" ::: "memory");
	s_add_i32 s17, s16, 1920
	s_min_u32 s17, s17, 0xfff
	s_lshr_b32 s18, s17, 5
	s_add_i32 s18, s18, 0
	s_and_b32 s19, s17, 31
	s_lshl_b32 s18, s18, 21
	s_lshl_b32 s19, s19, 9
	s_add_u32 s18, s18, s19
	s_add_u32 s12, s2, s18
	s_addc_u32 s13, s3, 0
	global_load_dwordx4 v[36:39], v10, s[12:13]
	s_add_u32 s12, s12, 0x8000
	s_addc_u32 s13, s13, 0
	global_load_dwordx4 v[40:43], v10, s[12:13]
	s_add_u32 s12, s12, 0x8000
	s_addc_u32 s13, s13, 0
	global_load_dwordx4 v[44:47], v10, s[12:13]
	s_add_u32 s12, s12, 0x8000
	s_addc_u32 s13, s13, 0
	global_load_dwordx4 v[48:51], v10, s[12:13]
	s_add_u32 s12, s12, 0x8000
	s_addc_u32 s13, s13, 0
	global_load_dwordx4 v[52:55], v10, s[12:13]
	s_add_u32 s12, s12, 0x8000
	s_addc_u32 s13, s13, 0
	global_load_dwordx4 v[56:59], v10, s[12:13]
	s_add_u32 s12, s12, 0x8000
	s_addc_u32 s13, s13, 0
	global_load_dwordx4 v[60:63], v10, s[12:13]
	s_add_u32 s12, s12, 0x8000
	s_addc_u32 s13, s13, 0
	global_load_dwordx4 v[64:67], v10, s[12:13]
	s_add_i32 s17, s16, 1536
	s_min_u32 s17, s17, 0xfff
	s_lshr_b32 s18, s17, 5
	s_add_i32 s18, s18, 0
	s_and_b32 s19, s17, 31
	s_lshl_b32 s19, s19, 21
	s_lshl_b32 s18, s18, 7
	s_add_u32 s18, s18, s19
	s_add_u32 s14, s4, s18
	s_addc_u32 s15, s5, 0
	ds_read_b32 v170, v6
	ds_read_b32 v171, v6 offset:512
	ds_read_b32 v172, v6 offset:1024
	ds_read_b32 v173, v6 offset:1536
	ds_read_b32 v174, v6 offset:2048
	ds_read_b32 v175, v6 offset:2560
	ds_read_b32 v176, v6 offset:3072
	ds_read_b32 v177, v6 offset:3584
	ds_read_b32 v196, v6 offset:4096
	ds_read_b32 v197, v6 offset:4608
	ds_read_b32 v198, v6 offset:5120
	ds_read_b32 v199, v6 offset:5632
	ds_read_b32 v200, v6 offset:6144
	ds_read_b32 v201, v6 offset:6656
	ds_read_b32 v202, v6 offset:7168
	ds_read_b32 v203, v6 offset:7680
	s_waitcnt lgkmcnt(0)
	v_max_f32_e32 v170, v170, v170
	v_max_f32_e32 v171, v171, v171
	v_max_f32_e32 v172, v172, v172
	v_max_f32_e32 v173, v173, v173
	v_max_f32_e32 v174, v174, v174
	v_max_f32_e32 v175, v175, v175
	v_max_f32_e32 v176, v176, v176
	v_max_f32_e32 v177, v177, v177
	v_max_f32_e32 v196, v196, v196
	v_max_f32_e32 v197, v197, v197
	v_max_f32_e32 v198, v198, v198
	v_max_f32_e32 v199, v199, v199
	v_max_f32_e32 v200, v200, v200
	v_max_f32_e32 v201, v201, v201
	v_max_f32_e32 v202, v202, v202
	v_max_f32_e32 v203, v203, v203
	v_med3_f32 v170, v170, s20, v13
	v_med3_f32 v171, v171, s20, v13
	v_med3_f32 v172, v172, s20, v13
	v_med3_f32 v173, v173, s20, v13
	v_med3_f32 v174, v174, s20, v13
	v_med3_f32 v175, v175, s20, v13
	v_med3_f32 v176, v176, s20, v13
	v_med3_f32 v177, v177, s20, v13
	v_med3_f32 v196, v196, s20, v13
	v_med3_f32 v197, v197, s20, v13
	v_med3_f32 v198, v198, s20, v13
	v_med3_f32 v199, v199, s20, v13
	v_med3_f32 v200, v200, s20, v13
	v_med3_f32 v201, v201, s20, v13
	v_med3_f32 v202, v202, s20, v13
	v_med3_f32 v203, v203, s20, v13
	v_mov_b32_e32 v208, 0
	v_mov_b32_e32 v209, 0
	v_mov_b32_e32 v210, 0
	v_mov_b32_e32 v211, 0
	v_cvt_pk_fp8_f32 v208, v170, v171
	v_cvt_pk_fp8_f32 v209, v174, v175
	v_cvt_pk_fp8_f32 v210, v196, v197
	v_cvt_pk_fp8_f32 v211, v200, v201
	v_cvt_pk_fp8_f32 v208, v172, v173 op_sel:[0,0,1]
	v_cvt_pk_fp8_f32 v209, v176, v177 op_sel:[0,0,1]
	v_cvt_pk_fp8_f32 v210, v198, v199 op_sel:[0,0,1]
	v_cvt_pk_fp8_f32 v211, v202, v203 op_sel:[0,0,1]
	s_nop 0
	global_store_dwordx4 v11, v[208:211], s[14:15]
	ds_read_b32 v170, v8
	ds_read_b32 v171, v8 offset:512
	ds_read_b32 v172, v8 offset:1024
	ds_read_b32 v173, v8 offset:1536
	ds_read_b32 v174, v8 offset:2048
	ds_read_b32 v175, v8 offset:2560
	ds_read_b32 v176, v8 offset:3072
	ds_read_b32 v177, v8 offset:3584
	ds_read_b32 v196, v8 offset:4096
	ds_read_b32 v197, v8 offset:4608
	ds_read_b32 v198, v8 offset:5120
	ds_read_b32 v199, v8 offset:5632
	ds_read_b32 v200, v8 offset:6144
	ds_read_b32 v201, v8 offset:6656
	ds_read_b32 v202, v8 offset:7168
	ds_read_b32 v203, v8 offset:7680
	s_waitcnt lgkmcnt(0)
	v_max_f32_e32 v170, v170, v170
	v_max_f32_e32 v171, v171, v171
	v_max_f32_e32 v172, v172, v172
	v_max_f32_e32 v173, v173, v173
	v_max_f32_e32 v174, v174, v174
	v_max_f32_e32 v175, v175, v175
	v_max_f32_e32 v176, v176, v176
	v_max_f32_e32 v177, v177, v177
	v_max_f32_e32 v196, v196, v196
	v_max_f32_e32 v197, v197, v197
	v_max_f32_e32 v198, v198, v198
	v_max_f32_e32 v199, v199, v199
	v_max_f32_e32 v200, v200, v200
	v_max_f32_e32 v201, v201, v201
	v_max_f32_e32 v202, v202, v202
	v_max_f32_e32 v203, v203, v203
	v_med3_f32 v170, v170, s20, v13
	v_med3_f32 v171, v171, s20, v13
	v_med3_f32 v172, v172, s20, v13
	v_med3_f32 v173, v173, s20, v13
	v_med3_f32 v174, v174, s20, v13
	v_med3_f32 v175, v175, s20, v13
	v_med3_f32 v176, v176, s20, v13
	v_med3_f32 v177, v177, s20, v13
	v_med3_f32 v196, v196, s20, v13
	v_med3_f32 v197, v197, s20, v13
	v_med3_f32 v198, v198, s20, v13
	v_med3_f32 v199, v199, s20, v13
	v_med3_f32 v200, v200, s20, v13
	v_med3_f32 v201, v201, s20, v13
	v_med3_f32 v202, v202, s20, v13
	v_med3_f32 v203, v203, s20, v13
	v_mov_b32_e32 v208, 0
	v_mov_b32_e32 v209, 0
	v_mov_b32_e32 v210, 0
	v_mov_b32_e32 v211, 0
	v_cvt_pk_fp8_f32 v208, v170, v171
	v_cvt_pk_fp8_f32 v209, v174, v175
	v_cvt_pk_fp8_f32 v210, v196, v197
	v_cvt_pk_fp8_f32 v211, v200, v201
	v_cvt_pk_fp8_f32 v208, v172, v173 op_sel:[0,0,1]
	v_cvt_pk_fp8_f32 v209, v176, v177 op_sel:[0,0,1]
	v_cvt_pk_fp8_f32 v210, v198, v199 op_sel:[0,0,1]
	v_cvt_pk_fp8_f32 v211, v202, v203 op_sel:[0,0,1]
	s_nop 0
	global_store_dwordx4 v12, v[208:211], s[14:15]
	s_waitcnt vmcnt(32)
	v_mul_f32_e32 v68, 0x43000000, v68
	v_mul_f32_e32 v69, 0x43000000, v69
	v_mul_f32_e32 v70, 0x43000000, v70
	v_mul_f32_e32 v71, 0x43000000, v71
	ds_write_b128 v5, v[68:71]
	v_mul_f32_e32 v72, 0x43000000, v72
	v_mul_f32_e32 v73, 0x43000000, v73
	v_mul_f32_e32 v74, 0x43000000, v74
	v_mul_f32_e32 v75, 0x43000000, v75
	ds_write_b128 v5, v[72:75] offset:1024
	v_mul_f32_e32 v76, 0x43000000, v76
	v_mul_f32_e32 v77, 0x43000000, v77
	v_mul_f32_e32 v78, 0x43000000, v78
	v_mul_f32_e32 v79, 0x43000000, v79
	ds_write_b128 v5, v[76:79] offset:2048
	v_mul_f32_e32 v80, 0x43000000, v80
	v_mul_f32_e32 v81, 0x43000000, v81
	v_mul_f32_e32 v82, 0x43000000, v82
	v_mul_f32_e32 v83, 0x43000000, v83
	ds_write_b128 v5, v[80:83] offset:3072
	v_mul_f32_e32 v84, 0x43000000, v84
	v_mul_f32_e32 v85, 0x43000000, v85
	v_mul_f32_e32 v86, 0x43000000, v86
	v_mul_f32_e32 v87, 0x43000000, v87
	ds_write_b128 v5, v[84:87] offset:4096
	v_mul_f32_e32 v88, 0x43000000, v88
	v_mul_f32_e32 v89, 0x43000000, v89
	v_mul_f32_e32 v90, 0x43000000, v90
	v_mul_f32_e32 v91, 0x43000000, v91
	ds_write_b128 v5, v[88:91] offset:5120
	v_mul_f32_e32 v92, 0x43000000, v92
	v_mul_f32_e32 v93, 0x43000000, v93
	v_mul_f32_e32 v94, 0x43000000, v94
	v_mul_f32_e32 v95, 0x43000000, v95
	ds_write_b128 v5, v[92:95] offset:6144
	v_mul_f32_e32 v96, 0x43000000, v96
	v_mul_f32_e32 v97, 0x43000000, v97
	v_mul_f32_e32 v98, 0x43000000, v98
	v_mul_f32_e32 v99, 0x43000000, v99
	ds_write_b128 v5, v[96:99] offset:7168
	s_waitcnt lgkmcnt(0)
	s_barrier
; #define GAS __attribute__((address_space(1)))
; #define LAS __attribute__((address_space(3)))
; #define LDS_WAIT() asm volatile("s_waitcnt lgkmcnt(0)" ::: "memory")
; __device__ __forceinline__ unsigned pk4_fp8(float a, float b, float c, float d) {
;     a = fminf(fmaxf(a, -448.f), 448.f); b = fminf(fmaxf(b, -448.f), 448.f); c = fminf(fmaxf(c, -448.f), 448.f); d = fminf(fmaxf(d, -448.f), 448.f);
;     int w = __builtin_amdgcn_cvt_pk_fp8_f32(a, b, 0, false); w = __builtin_amdgcn_cvt_pk_fp8_f32(c, d, w, true); return (unsigned)w; }
;     const int pr = item >> 1, kb = 2 * (pr / nblk) + (item & 1), nb = pr % nblk, k0 = 64 * kb, n0 = 32 * nb;
;     const int nr = n0 + (lane & 31); const int sc = MAP == 1 ? src_col_in(nr) : nr;
;     float v[32];
; #pragma unroll
;     for (int i = 0; i < 32; ++i) v[i] = sc >= 0 ? W[(size_t)(k0 + 2 * i + (lane >> 5)) * Nsrc + sc] : 0.f;
; #pragma unroll
;     for (int i = 0; i < 32; ++i) { const int k = k0 + 2 * i + (lane >> 5); float x = v[i] * wscale; if (KS) x *= (k < ksplit ? ksA[k] : ksB[k - ksplit]); scr[(2 * i + (lane >> 5)) * 33 + (lane & 31)] = x; }
;     LDS_WAIT(); asm volatile("" ::: "memory");
;     const int c = lane & 7;
; #pragma unroll
;     for (int j = 0; j < 4; ++j) { const int n = (lane >> 3) + 8 * j; const LAS float* s = scr + (8 * c) * 33 + n;
;         const unsigned long long o = (unsigned long long)pg8::pk4_fp8(s[0 * 33], s[1 * 33], s[2 * 33], s[3 * 33]) | ((unsigned long long)pg8::pk4_fp8(s[4 * 33], s[5 * 33], s[6 * 33], s[7 * 33]) << 32);
;         *(GAS unsigned long long*)(WT + (size_t)(n0 + n) * K + k0 + 8 * c) = o; }
;     LDS_WAIT(); asm volatile("" ::: "memory");
	s_add_i32 s17, s16, 2016
	s_min_u32 s17, s17, 0xfff
	s_lshr_b32 s18, s17, 5
	s_add_i32 s18, s18, 0
	s_and_b32 s19, s17, 31
	s_lshl_b32 s18, s18, 21
	s_lshl_b32 s19, s19, 9
	s_add_u32 s18, s18, s19
	s_add_u32 s12, s2, s18
	s_addc_u32 s13, s3, 0
	global_load_dwordx4 v[68:71], v10, s[12:13]
	s_add_u32 s12, s12, 0x8000
	s_addc_u32 s13, s13, 0
	global_load_dwordx4 v[72:75], v10, s[12:13]
	s_add_u32 s12, s12, 0x8000
	s_addc_u32 s13, s13, 0
	global_load_dwordx4 v[76:79], v10, s[12:13]
	s_add_u32 s12, s12, 0x8000
	s_addc_u32 s13, s13, 0
	global_load_dwordx4 v[80:83], v10, s[12:13]
	s_add_u32 s12, s12, 0x8000
	s_addc_u32 s13, s13, 0
	global_load_dwordx4 v[84:87], v10, s[12:13]
	s_add_u32 s12, s12, 0x8000
	s_addc_u32 s13, s13, 0
	global_load_dwordx4 v[88:91], v10, s[12:13]
	s_add_u32 s12, s12, 0x8000
	s_addc_u32 s13, s13, 0
	global_load_dwordx4 v[92:95], v10, s[12:13]
	s_add_u32 s12, s12, 0x8000
	s_addc_u32 s13, s13, 0
	global_load_dwordx4 v[96:99], v10, s[12:13]
	s_add_i32 s17, s16, 1632
	s_min_u32 s17, s17, 0xfff
	s_lshr_b32 s18, s17, 5
	s_add_i32 s18, s18, 0
	s_and_b32 s19, s17, 31
	s_lshl_b32 s19, s19, 21
	s_lshl_b32 s18, s18, 7
	s_add_u32 s18, s18, s19
	s_add_u32 s14, s4, s18
	s_addc_u32 s15, s5, 0
	ds_read_b32 v170, v7
	ds_read_b32 v171, v7 offset:512
	ds_read_b32 v172, v7 offset:1024
	ds_read_b32 v173, v7 offset:1536
	ds_read_b32 v174, v7 offset:2048
	ds_read_b32 v175, v7 offset:2560
	ds_read_b32 v176, v7 offset:3072
	ds_read_b32 v177, v7 offset:3584
	ds_read_b32 v196, v7 offset:4096
	ds_read_b32 v197, v7 offset:4608
	ds_read_b32 v198, v7 offset:5120
	ds_read_b32 v199, v7 offset:5632
	ds_read_b32 v200, v7 offset:6144
	ds_read_b32 v201, v7 offset:6656
	ds_read_b32 v202, v7 offset:7168
	ds_read_b32 v203, v7 offset:7680
	s_waitcnt lgkmcnt(0)
	v_max_f32_e32 v170, v170, v170
	v_max_f32_e32 v171, v171, v171
	v_max_f32_e32 v172, v172, v172
	v_max_f32_e32 v173, v173, v173
	v_max_f32_e32 v174, v174, v174
	v_max_f32_e32 v175, v175, v175
	v_max_f32_e32 v176, v176, v176
	v_max_f32_e32 v177, v177, v177
	v_max_f32_e32 v196, v196, v196
	v_max_f32_e32 v197, v197, v197
	v_max_f32_e32 v198, v198, v198
	v_max_f32_e32 v199, v199, v199
	v_max_f32_e32 v200, v200, v200
	v_max_f32_e32 v201, v201, v201
	v_max_f32_e32 v202, v202, v202
	v_max_f32_e32 v203, v203, v203
	v_med3_f32 v170, v170, s20, v13
	v_med3_f32 v171, v171, s20, v13
	v_med3_f32 v172, v172, s20, v13
	v_med3_f32 v173, v173, s20, v13
	v_med3_f32 v174, v174, s20, v13
	v_med3_f32 v175, v175, s20, v13
	v_med3_f32 v176, v176, s20, v13
	v_med3_f32 v177, v177, s20, v13
	v_med3_f32 v196, v196, s20, v13
	v_med3_f32 v197, v197, s20, v13
	v_med3_f32 v198, v198, s20, v13
	v_med3_f32 v199, v199, s20, v13
	v_med3_f32 v200, v200, s20, v13
	v_med3_f32 v201, v201, s20, v13
	v_med3_f32 v202, v202, s20, v13
	v_med3_f32 v203, v203, s20, v13
	v_mov_b32_e32 v208, 0
	v_mov_b32_e32 v209, 0
	v_mov_b32_e32 v210, 0
	v_mov_b32_e32 v211, 0
	v_cvt_pk_fp8_f32 v208, v170, v171
	v_cvt_pk_fp8_f32 v209, v174, v175
	v_cvt_pk_fp8_f32 v210, v196, v197
	v_cvt_pk_fp8_f32 v211, v200, v201
	v_cvt_pk_fp8_f32 v208, v172, v173 op_sel:[0,0,1]
	v_cvt_pk_fp8_f32 v209, v176, v177 op_sel:[0,0,1]
	v_cvt_pk_fp8_f32 v210, v198, v199 op_sel:[0,0,1]
	v_cvt_pk_fp8_f32 v211, v202, v203 op_sel:[0,0,1]
	s_nop 0
	global_store_dwordx4 v11, v[208:211], s[14:15]
	ds_read_b32 v170, v9
	ds_read_b32 v171, v9 offset:512
	ds_read_b32 v172, v9 offset:1024
	ds_read_b32 v173, v9 offset:1536
	ds_read_b32 v174, v9 offset:2048
	ds_read_b32 v175, v9 offset:2560
	ds_read_b32 v176, v9 offset:3072
	ds_read_b32 v177, v9 offset:3584
	ds_read_b32 v196, v9 offset:4096
	ds_read_b32 v197, v9 offset:4608
	ds_read_b32 v198, v9 offset:5120
	ds_read_b32 v199, v9 offset:5632
	ds_read_b32 v200, v9 offset:6144
	ds_read_b32 v201, v9 offset:6656
	ds_read_b32 v202, v9 offset:7168
	ds_read_b32 v203, v9 offset:7680
	s_waitcnt lgkmcnt(0)
	v_max_f32_e32 v170, v170, v170
	v_max_f32_e32 v171, v171, v171
	v_max_f32_e32 v172, v172, v172
	v_max_f32_e32 v173, v173, v173
	v_max_f32_e32 v174, v174, v174
	v_max_f32_e32 v175, v175, v175
	v_max_f32_e32 v176, v176, v176
	v_max_f32_e32 v177, v177, v177
	v_max_f32_e32 v196, v196, v196
	v_max_f32_e32 v197, v197, v197
	v_max_f32_e32 v198, v198, v198
	v_max_f32_e32 v199, v199, v199
	v_max_f32_e32 v200, v200, v200
	v_max_f32_e32 v201, v201, v201
	v_max_f32_e32 v202, v202, v202
	v_max_f32_e32 v203, v203, v203
	v_med3_f32 v170, v170, s20, v13
	v_med3_f32 v171, v171, s20, v13
	v_med3_f32 v172, v172, s20, v13
	v_med3_f32 v173, v173, s20, v13
	v_med3_f32 v174, v174, s20, v13
	v_med3_f32 v175, v175, s20, v13
	v_med3_f32 v176, v176, s20, v13
	v_med3_f32 v177, v177, s20, v13
	v_med3_f32 v196, v196, s20, v13
	v_med3_f32 v197, v197, s20, v13
	v_med3_f32 v198, v198, s20, v13
	v_med3_f32 v199, v199, s20, v13
	v_med3_f32 v200, v200, s20, v13
	v_med3_f32 v201, v201, s20, v13
	v_med3_f32 v202, v202, s20, v13
	v_med3_f32 v203, v203, s20, v13
	v_mov_b32_e32 v208, 0
	v_mov_b32_e32 v209, 0
	v_mov_b32_e32 v210, 0
	v_mov_b32_e32 v211, 0
	v_cvt_pk_fp8_f32 v208, v170, v171
	v_cvt_pk_fp8_f32 v209, v174, v175
	v_cvt_pk_fp8_f32 v210, v196, v197
	v_cvt_pk_fp8_f32 v211, v200, v201
	v_cvt_pk_fp8_f32 v208, v172, v173 op_sel:[0,0,1]
	v_cvt_pk_fp8_f32 v209, v176, v177 op_sel:[0,0,1]
	v_cvt_pk_fp8_f32 v210, v198, v199 op_sel:[0,0,1]
	v_cvt_pk_fp8_f32 v211, v202, v203 op_sel:[0,0,1]
	s_nop 0
	global_store_dwordx4 v12, v[208:211], s[14:15]
	s_waitcnt vmcnt(32)
	v_mul_f32_e32 v100, 0x43000000, v100
	v_mul_f32_e32 v101, 0x43000000, v101
	v_mul_f32_e32 v102, 0x43000000, v102
	v_mul_f32_e32 v103, 0x43000000, v103
	ds_write_b128 v4, v[100:103]
	v_mul_f32_e32 v104, 0x43000000, v104
	v_mul_f32_e32 v105, 0x43000000, v105
	v_mul_f32_e32 v106, 0x43000000, v106
	v_mul_f32_e32 v107, 0x43000000, v107
	ds_write_b128 v4, v[104:107] offset:1024
	v_mul_f32_e32 v108, 0x43000000, v108
	v_mul_f32_e32 v109, 0x43000000, v109
	v_mul_f32_e32 v110, 0x43000000, v110
	v_mul_f32_e32 v111, 0x43000000, v111
	ds_write_b128 v4, v[108:111] offset:2048
	v_mul_f32_e32 v112, 0x43000000, v112
	v_mul_f32_e32 v113, 0x43000000, v113
	v_mul_f32_e32 v114, 0x43000000, v114
	v_mul_f32_e32 v115, 0x43000000, v115
	ds_write_b128 v4, v[112:115] offset:3072
	v_mul_f32_e32 v116, 0x43000000, v116
	v_mul_f32_e32 v117, 0x43000000, v117
	v_mul_f32_e32 v118, 0x43000000, v118
	v_mul_f32_e32 v119, 0x43000000, v119
	ds_write_b128 v4, v[116:119] offset:4096
	v_mul_f32_e32 v120, 0x43000000, v120
	v_mul_f32_e32 v121, 0x43000000, v121
	v_mul_f32_e32 v122, 0x43000000, v122
	v_mul_f32_e32 v123, 0x43000000, v123
	ds_write_b128 v4, v[120:123] offset:5120
	v_mul_f32_e32 v124, 0x43000000, v124
	v_mul_f32_e32 v125, 0x43000000, v125
	v_mul_f32_e32 v126, 0x43000000, v126
	v_mul_f32_e32 v127, 0x43000000, v127
	ds_write_b128 v4, v[124:127] offset:6144
	v_mul_f32_e32 v128, 0x43000000, v128
	v_mul_f32_e32 v129, 0x43000000, v129
	v_mul_f32_e32 v130, 0x43000000, v130
	v_mul_f32_e32 v131, 0x43000000, v131
	ds_write_b128 v4, v[128:131] offset:7168
	s_waitcnt lgkmcnt(0)
	s_barrier
; #define GAS __attribute__((address_space(1)))
; #define LAS __attribute__((address_space(3)))
; #define LDS_WAIT() asm volatile("s_waitcnt lgkmcnt(0)" ::: "memory")
; __device__ __forceinline__ unsigned pk4_fp8(float a, float b, float c, float d) {
;     a = fminf(fmaxf(a, -448.f), 448.f); b = fminf(fmaxf(b, -448.f), 448.f); c = fminf(fmaxf(c, -448.f), 448.f); d = fminf(fmaxf(d, -448.f), 448.f);
;     int w = __builtin_amdgcn_cvt_pk_fp8_f32(a, b, 0, false); w = __builtin_amdgcn_cvt_pk_fp8_f32(c, d, w, true); return (unsigned)w; }
;     const int pr = item >> 1, kb = 2 * (pr / nblk) + (item & 1), nb = pr % nblk, k0 = 64 * kb, n0 = 32 * nb;
;     const int nr = n0 + (lane & 31); const int sc = MAP == 1 ? src_col_in(nr) : nr;
;     float v[32];
; #pragma unroll
;     for (int i = 0; i < 32; ++i) v[i] = sc >= 0 ? W[(size_t)(k0 + 2 * i + (lane >> 5)) * Nsrc + sc] : 0.f;
; #pragma unroll
;     for (int i = 0; i < 32; ++i) { const int k = k0 + 2 * i + (lane >> 5); float x = v[i] * wscale; if (KS) x *= (k < ksplit ? ksA[k] : ksB[k - ksplit]); scr[(2 * i + (lane >> 5)) * 33 + (lane & 31)] = x; }
;     LDS_WAIT(); asm volatile("" ::: "memory");
;     const int c = lane & 7;
; #pragma unroll
;     for (int j = 0; j < 4; ++j) { const int n = (lane >> 3) + 8 * j; const LAS float* s = scr + (8 * c) * 33 + n;
;         const unsigned long long o = (unsigned long long)pg8::pk4_fp8(s[0 * 33], s[1 * 33], s[2 * 33], s[3 * 33]) | ((unsigned long long)pg8::pk4_fp8(s[4 * 33], s[5 * 33], s[6 * 33], s[7 * 33]) << 32);
;         *(GAS unsigned long long*)(WT + (size_t)(n0 + n) * K + k0 + 8 * c) = o; }
;     LDS_WAIT(); asm volatile("" ::: "memory");
	s_add_i32 s17, s16, 2112
	s_min_u32 s17, s17, 0xfff
	s_lshr_b32 s18, s17, 5
	s_add_i32 s18, s18, 0
	s_and_b32 s19, s17, 31
	s_lshl_b32 s18, s18, 21
	s_lshl_b32 s19, s19, 9
	s_add_u32 s18, s18, s19
	s_add_u32 s12, s2, s18
	s_addc_u32 s13, s3, 0
	global_load_dwordx4 v[100:103], v10, s[12:13]
	s_add_u32 s12, s12, 0x8000
	s_addc_u32 s13, s13, 0
	global_load_dwordx4 v[104:107], v10, s[12:13]
	s_add_u32 s12, s12, 0x8000
	s_addc_u32 s13, s13, 0
	global_load_dwordx4 v[108:111], v10, s[12:13]
	s_add_u32 s12, s12, 0x8000
	s_addc_u32 s13, s13, 0
	global_load_dwordx4 v[112:115], v10, s[12:13]
	s_add_u32 s12, s12, 0x8000
	s_addc_u32 s13, s13, 0
	global_load_dwordx4 v[116:119], v10, s[12:13]
	s_add_u32 s12, s12, 0x8000
	s_addc_u32 s13, s13, 0
	global_load_dwordx4 v[120:123], v10, s[12:13]
	s_add_u32 s12, s12, 0x8000
	s_addc_u32 s13, s13, 0
	global_load_dwordx4 v[124:127], v10, s[12:13]
	s_add_u32 s12, s12, 0x8000
	s_addc_u32 s13, s13, 0
	global_load_dwordx4 v[128:131], v10, s[12:13]
	s_add_i32 s17, s16, 1728
	s_min_u32 s17, s17, 0xfff
	s_lshr_b32 s18, s17, 5
	s_add_i32 s18, s18, 0
	s_and_b32 s19, s17, 31
	s_lshl_b32 s19, s19, 21
	s_lshl_b32 s18, s18, 7
	s_add_u32 s18, s18, s19
	s_add_u32 s14, s4, s18
	s_addc_u32 s15, s5, 0
	ds_read_b32 v170, v6
	ds_read_b32 v171, v6 offset:512
	ds_read_b32 v172, v6 offset:1024
	ds_read_b32 v173, v6 offset:1536
	ds_read_b32 v174, v6 offset:2048
	ds_read_b32 v175, v6 offset:2560
	ds_read_b32 v176, v6 offset:3072
	ds_read_b32 v177, v6 offset:3584
	ds_read_b32 v196, v6 offset:4096
	ds_read_b32 v197, v6 offset:4608
	ds_read_b32 v198, v6 offset:5120
	ds_read_b32 v199, v6 offset:5632
	ds_read_b32 v200, v6 offset:6144
	ds_read_b32 v201, v6 offset:6656
	ds_read_b32 v202, v6 offset:7168
	ds_read_b32 v203, v6 offset:7680
	s_waitcnt lgkmcnt(0)
	v_max_f32_e32 v170, v170, v170
	v_max_f32_e32 v171, v171, v171
	v_max_f32_e32 v172, v172, v172
	v_max_f32_e32 v173, v173, v173
	v_max_f32_e32 v174, v174, v174
	v_max_f32_e32 v175, v175, v175
	v_max_f32_e32 v176, v176, v176
	v_max_f32_e32 v177, v177, v177
	v_max_f32_e32 v196, v196, v196
	v_max_f32_e32 v197, v197, v197
	v_max_f32_e32 v198, v198, v198
	v_max_f32_e32 v199, v199, v199
	v_max_f32_e32 v200, v200, v200
	v_max_f32_e32 v201, v201, v201
	v_max_f32_e32 v202, v202, v202
	v_max_f32_e32 v203, v203, v203
	v_med3_f32 v170, v170, s20, v13
	v_med3_f32 v171, v171, s20, v13
	v_med3_f32 v172, v172, s20, v13
	v_med3_f32 v173, v173, s20, v13
	v_med3_f32 v174, v174, s20, v13
	v_med3_f32 v175, v175, s20, v13
	v_med3_f32 v176, v176, s20, v13
	v_med3_f32 v177, v177, s20, v13
	v_med3_f32 v196, v196, s20, v13
	v_med3_f32 v197, v197, s20, v13
	v_med3_f32 v198, v198, s20, v13
	v_med3_f32 v199, v199, s20, v13
	v_med3_f32 v200, v200, s20, v13
	v_med3_f32 v201, v201, s20, v13
	v_med3_f32 v202, v202, s20, v13
	v_med3_f32 v203, v203, s20, v13
	v_mov_b32_e32 v208, 0
	v_mov_b32_e32 v209, 0
	v_mov_b32_e32 v210, 0
	v_mov_b32_e32 v211, 0
	v_cvt_pk_fp8_f32 v208, v170, v171
	v_cvt_pk_fp8_f32 v209, v174, v175
	v_cvt_pk_fp8_f32 v210, v196, v197
	v_cvt_pk_fp8_f32 v211, v200, v201
	v_cvt_pk_fp8_f32 v208, v172, v173 op_sel:[0,0,1]
	v_cvt_pk_fp8_f32 v209, v176, v177 op_sel:[0,0,1]
	v_cvt_pk_fp8_f32 v210, v198, v199 op_sel:[0,0,1]
	v_cvt_pk_fp8_f32 v211, v202, v203 op_sel:[0,0,1]
	s_nop 0
	global_store_dwordx4 v11, v[208:211], s[14:15]
	ds_read_b32 v170, v8
	ds_read_b32 v171, v8 offset:512
	ds_read_b32 v172, v8 offset:1024
	ds_read_b32 v173, v8 offset:1536
	ds_read_b32 v174, v8 offset:2048
	ds_read_b32 v175, v8 offset:2560
	ds_read_b32 v176, v8 offset:3072
	ds_read_b32 v177, v8 offset:3584
	ds_read_b32 v196, v8 offset:4096
	ds_read_b32 v197, v8 offset:4608
	ds_read_b32 v198, v8 offset:5120
	ds_read_b32 v199, v8 offset:5632
	ds_read_b32 v200, v8 offset:6144
	ds_read_b32 v201, v8 offset:6656
	ds_read_b32 v202, v8 offset:7168
	ds_read_b32 v203, v8 offset:7680
	s_waitcnt lgkmcnt(0)
	v_max_f32_e32 v170, v170, v170
	v_max_f32_e32 v171, v171, v171
	v_max_f32_e32 v172, v172, v172
	v_max_f32_e32 v173, v173, v173
	v_max_f32_e32 v174, v174, v174
	v_max_f32_e32 v175, v175, v175
	v_max_f32_e32 v176, v176, v176
	v_max_f32_e32 v177, v177, v177
	v_max_f32_e32 v196, v196, v196
	v_max_f32_e32 v197, v197, v197
	v_max_f32_e32 v198, v198, v198
	v_max_f32_e32 v199, v199, v199
	v_max_f32_e32 v200, v200, v200
	v_max_f32_e32 v201, v201, v201
	v_max_f32_e32 v202, v202, v202
	v_max_f32_e32 v203, v203, v203
	v_med3_f32 v170, v170, s20, v13
	v_med3_f32 v171, v171, s20, v13
	v_med3_f32 v172, v172, s20, v13
	v_med3_f32 v173, v173, s20, v13
	v_med3_f32 v174, v174, s20, v13
	v_med3_f32 v175, v175, s20, v13
	v_med3_f32 v176, v176, s20, v13
	v_med3_f32 v177, v177, s20, v13
	v_med3_f32 v196, v196, s20, v13
	v_med3_f32 v197, v197, s20, v13
	v_med3_f32 v198, v198, s20, v13
	v_med3_f32 v199, v199, s20, v13
	v_med3_f32 v200, v200, s20, v13
	v_med3_f32 v201, v201, s20, v13
	v_med3_f32 v202, v202, s20, v13
	v_med3_f32 v203, v203, s20, v13
	v_mov_b32_e32 v208, 0
	v_mov_b32_e32 v209, 0
	v_mov_b32_e32 v210, 0
	v_mov_b32_e32 v211, 0
	v_cvt_pk_fp8_f32 v208, v170, v171
	v_cvt_pk_fp8_f32 v209, v174, v175
	v_cvt_pk_fp8_f32 v210, v196, v197
	v_cvt_pk_fp8_f32 v211, v200, v201
	v_cvt_pk_fp8_f32 v208, v172, v173 op_sel:[0,0,1]
	v_cvt_pk_fp8_f32 v209, v176, v177 op_sel:[0,0,1]
	v_cvt_pk_fp8_f32 v210, v198, v199 op_sel:[0,0,1]
	v_cvt_pk_fp8_f32 v211, v202, v203 op_sel:[0,0,1]
	s_nop 0
	global_store_dwordx4 v12, v[208:211], s[14:15]
	s_waitcnt vmcnt(32)
	v_mul_f32_e32 v132, 0x43000000, v132
	v_mul_f32_e32 v133, 0x43000000, v133
	v_mul_f32_e32 v134, 0x43000000, v134
	v_mul_f32_e32 v135, 0x43000000, v135
	ds_write_b128 v5, v[132:135]
	v_mul_f32_e32 v136, 0x43000000, v136
	v_mul_f32_e32 v137, 0x43000000, v137
	v_mul_f32_e32 v138, 0x43000000, v138
	v_mul_f32_e32 v139, 0x43000000, v139
	ds_write_b128 v5, v[136:139] offset:1024
	v_mul_f32_e32 v140, 0x43000000, v140
	v_mul_f32_e32 v141, 0x43000000, v141
	v_mul_f32_e32 v142, 0x43000000, v142
	v_mul_f32_e32 v143, 0x43000000, v143
	ds_write_b128 v5, v[140:143] offset:2048
	v_mul_f32_e32 v144, 0x43000000, v144
	v_mul_f32_e32 v145, 0x43000000, v145
	v_mul_f32_e32 v146, 0x43000000, v146
	v_mul_f32_e32 v147, 0x43000000, v147
	ds_write_b128 v5, v[144:147] offset:3072
	v_mul_f32_e32 v148, 0x43000000, v148
	v_mul_f32_e32 v149, 0x43000000, v149
	v_mul_f32_e32 v150, 0x43000000, v150
	v_mul_f32_e32 v151, 0x43000000, v151
	ds_write_b128 v5, v[148:151] offset:4096
	v_mul_f32_e32 v152, 0x43000000, v152
	v_mul_f32_e32 v153, 0x43000000, v153
	v_mul_f32_e32 v154, 0x43000000, v154
	v_mul_f32_e32 v155, 0x43000000, v155
	ds_write_b128 v5, v[152:155] offset:5120
	v_mul_f32_e32 v156, 0x43000000, v156
	v_mul_f32_e32 v157, 0x43000000, v157
	v_mul_f32_e32 v158, 0x43000000, v158
	v_mul_f32_e32 v159, 0x43000000, v159
	ds_write_b128 v5, v[156:159] offset:6144
	v_mul_f32_e32 v160, 0x43000000, v160
	v_mul_f32_e32 v161, 0x43000000, v161
	v_mul_f32_e32 v162, 0x43000000, v162
	v_mul_f32_e32 v163, 0x43000000, v163
	ds_write_b128 v5, v[160:163] offset:7168
	s_waitcnt lgkmcnt(0)
	s_barrier
; #define GAS __attribute__((address_space(1)))
; #define LAS __attribute__((address_space(3)))
; #define LDS_WAIT() asm volatile("s_waitcnt lgkmcnt(0)" ::: "memory")
; __device__ __forceinline__ unsigned pk4_fp8(float a, float b, float c, float d) {
;     a = fminf(fmaxf(a, -448.f), 448.f); b = fminf(fmaxf(b, -448.f), 448.f); c = fminf(fmaxf(c, -448.f), 448.f); d = fminf(fmaxf(d, -448.f), 448.f);
;     int w = __builtin_amdgcn_cvt_pk_fp8_f32(a, b, 0, false); w = __builtin_amdgcn_cvt_pk_fp8_f32(c, d, w, true); return (unsigned)w; }
;     const int pr = item >> 1, kb = 2 * (pr / nblk) + (item & 1), nb = pr % nblk, k0 = 64 * kb, n0 = 32 * nb;
;     const int nr = n0 + (lane & 31); const int sc = MAP == 1 ? src_col_in(nr) : nr;
;     float v[32];
; #pragma unroll
;     for (int i = 0; i < 32; ++i) v[i] = sc >= 0 ? W[(size_t)(k0 + 2 * i + (lane >> 5)) * Nsrc + sc] : 0.f;
; #pragma unroll
;     for (int i = 0; i < 32; ++i) { const int k = k0 + 2 * i + (lane >> 5); float x = v[i] * wscale; if (KS) x *= (k < ksplit ? ksA[k] : ksB[k - ksplit]); scr[(2 * i + (lane >> 5)) * 33 + (lane & 31)] = x; }
;     LDS_WAIT(); asm volatile("" ::: "memory");
;     const int c = lane & 7;
; #pragma unroll
;     for (int j = 0; j < 4; ++j) { const int n = (lane >> 3) + 8 * j; const LAS float* s = scr + (8 * c) * 33 + n;
;         const unsigned long long o = (unsigned long long)pg8::pk4_fp8(s[0 * 33], s[1 * 33], s[2 * 33], s[3 * 33]) | ((unsigned long long)pg8::pk4_fp8(s[4 * 33], s[5 * 33], s[6 * 33], s[7 * 33]) << 32);
;         *(GAS unsigned long long*)(WT + (size_t)(n0 + n) * K + k0 + 8 * c) = o; }
;     LDS_WAIT(); asm volatile("" ::: "memory");
	s_add_i32 s17, s16, 2208
	s_min_u32 s17, s17, 0xfff
	s_lshr_b32 s18, s17, 5
	s_add_i32 s18, s18, 0
	s_and_b32 s19, s17, 31
	s_lshl_b32 s18, s18, 21
	s_lshl_b32 s19, s19, 9
	s_add_u32 s18, s18, s19
	s_add_u32 s12, s2, s18
	s_addc_u32 s13, s3, 0
	global_load_dwordx4 v[132:135], v10, s[12:13]
	s_add_u32 s12, s12, 0x8000
	s_addc_u32 s13, s13, 0
	global_load_dwordx4 v[136:139], v10, s[12:13]
	s_add_u32 s12, s12, 0x8000
	s_addc_u32 s13, s13, 0
	global_load_dwordx4 v[140:143], v10, s[12:13]
	s_add_u32 s12, s12, 0x8000
	s_addc_u32 s13, s13, 0
	global_load_dwordx4 v[144:147], v10, s[12:13]
	s_add_u32 s12, s12, 0x8000
	s_addc_u32 s13, s13, 0
	global_load_dwordx4 v[148:151], v10, s[12:13]
	s_add_u32 s12, s12, 0x8000
	s_addc_u32 s13, s13, 0
	global_load_dwordx4 v[152:155], v10, s[12:13]
	s_add_u32 s12, s12, 0x8000
	s_addc_u32 s13, s13, 0
	global_load_dwordx4 v[156:159], v10, s[12:13]
	s_add_u32 s12, s12, 0x8000
	s_addc_u32 s13, s13, 0
	global_load_dwordx4 v[160:163], v10, s[12:13]
	s_add_i32 s17, s16, 1824
	s_min_u32 s17, s17, 0xfff
	s_lshr_b32 s18, s17, 5
	s_add_i32 s18, s18, 0
	s_and_b32 s19, s17, 31
	s_lshl_b32 s19, s19, 21
	s_lshl_b32 s18, s18, 7
	s_add_u32 s18, s18, s19
	s_add_u32 s14, s4, s18
	s_addc_u32 s15, s5, 0
	ds_read_b32 v170, v7
	ds_read_b32 v171, v7 offset:512
	ds_read_b32 v172, v7 offset:1024
	ds_read_b32 v173, v7 offset:1536
	ds_read_b32 v174, v7 offset:2048
	ds_read_b32 v175, v7 offset:2560
	ds_read_b32 v176, v7 offset:3072
	ds_read_b32 v177, v7 offset:3584
	ds_read_b32 v196, v7 offset:4096
	ds_read_b32 v197, v7 offset:4608
	ds_read_b32 v198, v7 offset:5120
	ds_read_b32 v199, v7 offset:5632
	ds_read_b32 v200, v7 offset:6144
	ds_read_b32 v201, v7 offset:6656
	ds_read_b32 v202, v7 offset:7168
	ds_read_b32 v203, v7 offset:7680
	s_waitcnt lgkmcnt(0)
	v_max_f32_e32 v170, v170, v170
	v_max_f32_e32 v171, v171, v171
	v_max_f32_e32 v172, v172, v172
	v_max_f32_e32 v173, v173, v173
	v_max_f32_e32 v174, v174, v174
	v_max_f32_e32 v175, v175, v175
	v_max_f32_e32 v176, v176, v176
	v_max_f32_e32 v177, v177, v177
	v_max_f32_e32 v196, v196, v196
	v_max_f32_e32 v197, v197, v197
	v_max_f32_e32 v198, v198, v198
	v_max_f32_e32 v199, v199, v199
	v_max_f32_e32 v200, v200, v200
	v_max_f32_e32 v201, v201, v201
	v_max_f32_e32 v202, v202, v202
	v_max_f32_e32 v203, v203, v203
	v_med3_f32 v170, v170, s20, v13
	v_med3_f32 v171, v171, s20, v13
	v_med3_f32 v172, v172, s20, v13
	v_med3_f32 v173, v173, s20, v13
	v_med3_f32 v174, v174, s20, v13
	v_med3_f32 v175, v175, s20, v13
	v_med3_f32 v176, v176, s20, v13
	v_med3_f32 v177, v177, s20, v13
	v_med3_f32 v196, v196, s20, v13
	v_med3_f32 v197, v197, s20, v13
	v_med3_f32 v198, v198, s20, v13
	v_med3_f32 v199, v199, s20, v13
	v_med3_f32 v200, v200, s20, v13
	v_med3_f32 v201, v201, s20, v13
	v_med3_f32 v202, v202, s20, v13
	v_med3_f32 v203, v203, s20, v13
	v_mov_b32_e32 v208, 0
	v_mov_b32_e32 v209, 0
	v_mov_b32_e32 v210, 0
	v_mov_b32_e32 v211, 0
	v_cvt_pk_fp8_f32 v208, v170, v171
	v_cvt_pk_fp8_f32 v209, v174, v175
	v_cvt_pk_fp8_f32 v210, v196, v197
	v_cvt_pk_fp8_f32 v211, v200, v201
	v_cvt_pk_fp8_f32 v208, v172, v173 op_sel:[0,0,1]
	v_cvt_pk_fp8_f32 v209, v176, v177 op_sel:[0,0,1]
	v_cvt_pk_fp8_f32 v210, v198, v199 op_sel:[0,0,1]
	v_cvt_pk_fp8_f32 v211, v202, v203 op_sel:[0,0,1]
	s_nop 0
	global_store_dwordx4 v11, v[208:211], s[14:15]
	ds_read_b32 v170, v9
	ds_read_b32 v171, v9 offset:512
	ds_read_b32 v172, v9 offset:1024
	ds_read_b32 v173, v9 offset:1536
	ds_read_b32 v174, v9 offset:2048
	ds_read_b32 v175, v9 offset:2560
	ds_read_b32 v176, v9 offset:3072
	ds_read_b32 v177, v9 offset:3584
	ds_read_b32 v196, v9 offset:4096
	ds_read_b32 v197, v9 offset:4608
	ds_read_b32 v198, v9 offset:5120
	ds_read_b32 v199, v9 offset:5632
	ds_read_b32 v200, v9 offset:6144
	ds_read_b32 v201, v9 offset:6656
	ds_read_b32 v202, v9 offset:7168
	ds_read_b32 v203, v9 offset:7680
	s_waitcnt lgkmcnt(0)
	v_max_f32_e32 v170, v170, v170
	v_max_f32_e32 v171, v171, v171
	v_max_f32_e32 v172, v172, v172
	v_max_f32_e32 v173, v173, v173
	v_max_f32_e32 v174, v174, v174
	v_max_f32_e32 v175, v175, v175
	v_max_f32_e32 v176, v176, v176
	v_max_f32_e32 v177, v177, v177
	v_max_f32_e32 v196, v196, v196
	v_max_f32_e32 v197, v197, v197
	v_max_f32_e32 v198, v198, v198
	v_max_f32_e32 v199, v199, v199
	v_max_f32_e32 v200, v200, v200
	v_max_f32_e32 v201, v201, v201
	v_max_f32_e32 v202, v202, v202
	v_max_f32_e32 v203, v203, v203
	v_med3_f32 v170, v170, s20, v13
	v_med3_f32 v171, v171, s20, v13
	v_med3_f32 v172, v172, s20, v13
	v_med3_f32 v173, v173, s20, v13
	v_med3_f32 v174, v174, s20, v13
	v_med3_f32 v175, v175, s20, v13
	v_med3_f32 v176, v176, s20, v13
	v_med3_f32 v177, v177, s20, v13
	v_med3_f32 v196, v196, s20, v13
	v_med3_f32 v197, v197, s20, v13
	v_med3_f32 v198, v198, s20, v13
	v_med3_f32 v199, v199, s20, v13
	v_med3_f32 v200, v200, s20, v13
	v_med3_f32 v201, v201, s20, v13
	v_med3_f32 v202, v202, s20, v13
	v_med3_f32 v203, v203, s20, v13
	v_mov_b32_e32 v208, 0
	v_mov_b32_e32 v209, 0
	v_mov_b32_e32 v210, 0
	v_mov_b32_e32 v211, 0
	v_cvt_pk_fp8_f32 v208, v170, v171
	v_cvt_pk_fp8_f32 v209, v174, v175
	v_cvt_pk_fp8_f32 v210, v196, v197
	v_cvt_pk_fp8_f32 v211, v200, v201
	v_cvt_pk_fp8_f32 v208, v172, v173 op_sel:[0,0,1]
	v_cvt_pk_fp8_f32 v209, v176, v177 op_sel:[0,0,1]
	v_cvt_pk_fp8_f32 v210, v198, v199 op_sel:[0,0,1]
	v_cvt_pk_fp8_f32 v211, v202, v203 op_sel:[0,0,1]
	s_nop 0
	global_store_dwordx4 v12, v[208:211], s[14:15]
	s_waitcnt vmcnt(32)
	v_mul_f32_e32 v36, 0x43000000, v36
	v_mul_f32_e32 v37, 0x43000000, v37
	v_mul_f32_e32 v38, 0x43000000, v38
	v_mul_f32_e32 v39, 0x43000000, v39
	ds_write_b128 v4, v[36:39]
	v_mul_f32_e32 v40, 0x43000000, v40
	v_mul_f32_e32 v41, 0x43000000, v41
	v_mul_f32_e32 v42, 0x43000000, v42
	v_mul_f32_e32 v43, 0x43000000, v43
	ds_write_b128 v4, v[40:43] offset:1024
	v_mul_f32_e32 v44, 0x43000000, v44
	v_mul_f32_e32 v45, 0x43000000, v45
	v_mul_f32_e32 v46, 0x43000000, v46
	v_mul_f32_e32 v47, 0x43000000, v47
	ds_write_b128 v4, v[44:47] offset:2048
	v_mul_f32_e32 v48, 0x43000000, v48
	v_mul_f32_e32 v49, 0x43000000, v49
	v_mul_f32_e32 v50, 0x43000000, v50
	v_mul_f32_e32 v51, 0x43000000, v51
	ds_write_b128 v4, v[48:51] offset:3072
	v_mul_f32_e32 v52, 0x43000000, v52
	v_mul_f32_e32 v53, 0x43000000, v53
	v_mul_f32_e32 v54, 0x43000000, v54
	v_mul_f32_e32 v55, 0x43000000, v55
	ds_write_b128 v4, v[52:55] offset:4096
	v_mul_f32_e32 v56, 0x43000000, v56
	v_mul_f32_e32 v57, 0x43000000, v57
	v_mul_f32_e32 v58, 0x43000000, v58
	v_mul_f32_e32 v59, 0x43000000, v59
	ds_write_b128 v4, v[56:59] offset:5120
	v_mul_f32_e32 v60, 0x43000000, v60
	v_mul_f32_e32 v61, 0x43000000, v61
	v_mul_f32_e32 v62, 0x43000000, v62
	v_mul_f32_e32 v63, 0x43000000, v63
	ds_write_b128 v4, v[60:63] offset:6144
	v_mul_f32_e32 v64, 0x43000000, v64
	v_mul_f32_e32 v65, 0x43000000, v65
	v_mul_f32_e32 v66, 0x43000000, v66
	v_mul_f32_e32 v67, 0x43000000, v67
	ds_write_b128 v4, v[64:67] offset:7168
	s_waitcnt lgkmcnt(0)
	s_barrier
; #define GAS __attribute__((address_space(1)))
; #define LAS __attribute__((address_space(3)))
; #define LDS_WAIT() asm volatile("s_waitcnt lgkmcnt(0)" ::: "memory")
; __device__ __forceinline__ unsigned pk4_fp8(float a, float b, float c, float d) {
;     a = fminf(fmaxf(a, -448.f), 448.f); b = fminf(fmaxf(b, -448.f), 448.f); c = fminf(fmaxf(c, -448.f), 448.f); d = fminf(fmaxf(d, -448.f), 448.f);
;     int w = __builtin_amdgcn_cvt_pk_fp8_f32(a, b, 0, false); w = __builtin_amdgcn_cvt_pk_fp8_f32(c, d, w, true); return (unsigned)w; }
;     const int pr = item >> 1, kb = 2 * (pr / nblk) + (item & 1), nb = pr % nblk, k0 = 64 * kb, n0 = 32 * nb;
;     const int nr = n0 + (lane & 31); const int sc = MAP == 1 ? src_col_in(nr) : nr;
;     float v[32];
; #pragma unroll
;     for (int i = 0; i < 32; ++i) v[i] = sc >= 0 ? W[(size_t)(k0 + 2 * i + (lane >> 5)) * Nsrc + sc] : 0.f;
; #pragma unroll
;     for (int i = 0; i < 32; ++i) { const int k = k0 + 2 * i + (lane >> 5); float x = v[i] * wscale; if (KS) x *= (k < ksplit ? ksA[k] : ksB[k - ksplit]); scr[(2 * i + (lane >> 5)) * 33 + (lane & 31)] = x; }
;     LDS_WAIT(); asm volatile("" ::: "memory");
;     const int c = lane & 7;
; #pragma unroll
;     for (int j = 0; j < 4; ++j) { const int n = (lane >> 3) + 8 * j; const LAS float* s = scr + (8 * c) * 33 + n;
;         const unsigned long long o = (unsigned long long)pg8::pk4_fp8(s[0 * 33], s[1 * 33], s[2 * 33], s[3 * 33]) | ((unsigned long long)pg8::pk4_fp8(s[4 * 33], s[5 * 33], s[6 * 33], s[7 * 33]) << 32);
;         *(GAS unsigned long long*)(WT + (size_t)(n0 + n) * K + k0 + 8 * c) = o; }
;     LDS_WAIT(); asm volatile("" ::: "memory");
	s_add_i32 s17, s16, 2304
	s_min_u32 s17, s17, 0xfff
	s_lshr_b32 s18, s17, 5
	s_add_i32 s18, s18, 0
	s_and_b32 s19, s17, 31
	s_lshl_b32 s18, s18, 21
	s_lshl_b32 s19, s19, 9
	s_add_u32 s18, s18, s19
	s_add_u32 s12, s2, s18
	s_addc_u32 s13, s3, 0
	global_load_dwordx4 v[36:39], v10, s[12:13]
	s_add_u32 s12, s12, 0x8000
	s_addc_u32 s13, s13, 0
	global_load_dwordx4 v[40:43], v10, s[12:13]
	s_add_u32 s12, s12, 0x8000
	s_addc_u32 s13, s13, 0
	global_load_dwordx4 v[44:47], v10, s[12:13]
	s_add_u32 s12, s12, 0x8000
	s_addc_u32 s13, s13, 0
	global_load_dwordx4 v[48:51], v10, s[12:13]
	s_add_u32 s12, s12, 0x8000
	s_addc_u32 s13, s13, 0
	global_load_dwordx4 v[52:55], v10, s[12:13]
	s_add_u32 s12, s12, 0x8000
	s_addc_u32 s13, s13, 0
	global_load_dwordx4 v[56:59], v10, s[12:13]
	s_add_u32 s12, s12, 0x8000
	s_addc_u32 s13, s13, 0
	global_load_dwordx4 v[60:63], v10, s[12:13]
	s_add_u32 s12, s12, 0x8000
	s_addc_u32 s13, s13, 0
	global_load_dwordx4 v[64:67], v10, s[12:13]
	s_add_i32 s17, s16, 1920
	s_min_u32 s17, s17, 0xfff
	s_lshr_b32 s18, s17, 5
	s_add_i32 s18, s18, 0
	s_and_b32 s19, s17, 31
	s_lshl_b32 s19, s19, 21
	s_lshl_b32 s18, s18, 7
	s_add_u32 s18, s18, s19
	s_add_u32 s14, s4, s18
	s_addc_u32 s15, s5, 0
	ds_read_b32 v170, v6
	ds_read_b32 v171, v6 offset:512
	ds_read_b32 v172, v6 offset:1024
	ds_read_b32 v173, v6 offset:1536
	ds_read_b32 v174, v6 offset:2048
	ds_read_b32 v175, v6 offset:2560
	ds_read_b32 v176, v6 offset:3072
	ds_read_b32 v177, v6 offset:3584
	ds_read_b32 v196, v6 offset:4096
	ds_read_b32 v197, v6 offset:4608
	ds_read_b32 v198, v6 offset:5120
	ds_read_b32 v199, v6 offset:5632
	ds_read_b32 v200, v6 offset:6144
	ds_read_b32 v201, v6 offset:6656
	ds_read_b32 v202, v6 offset:7168
	ds_read_b32 v203, v6 offset:7680
	s_waitcnt lgkmcnt(0)
	v_max_f32_e32 v170, v170, v170
	v_max_f32_e32 v171, v171, v171
	v_max_f32_e32 v172, v172, v172
	v_max_f32_e32 v173, v173, v173
	v_max_f32_e32 v174, v174, v174
	v_max_f32_e32 v175, v175, v175
	v_max_f32_e32 v176, v176, v176
	v_max_f32_e32 v177, v177, v177
	v_max_f32_e32 v196, v196, v196
	v_max_f32_e32 v197, v197, v197
	v_max_f32_e32 v198, v198, v198
	v_max_f32_e32 v199, v199, v199
	v_max_f32_e32 v200, v200, v200
	v_max_f32_e32 v201, v201, v201
	v_max_f32_e32 v202, v202, v202
	v_max_f32_e32 v203, v203, v203
	v_med3_f32 v170, v170, s20, v13
	v_med3_f32 v171, v171, s20, v13
	v_med3_f32 v172, v172, s20, v13
	v_med3_f32 v173, v173, s20, v13
	v_med3_f32 v174, v174, s20, v13
	v_med3_f32 v175, v175, s20, v13
	v_med3_f32 v176, v176, s20, v13
	v_med3_f32 v177, v177, s20, v13
	v_med3_f32 v196, v196, s20, v13
	v_med3_f32 v197, v197, s20, v13
	v_med3_f32 v198, v198, s20, v13
	v_med3_f32 v199, v199, s20, v13
	v_med3_f32 v200, v200, s20, v13
	v_med3_f32 v201, v201, s20, v13
	v_med3_f32 v202, v202, s20, v13
	v_med3_f32 v203, v203, s20, v13
	v_mov_b32_e32 v208, 0
	v_mov_b32_e32 v209, 0
	v_mov_b32_e32 v210, 0
	v_mov_b32_e32 v211, 0
	v_cvt_pk_fp8_f32 v208, v170, v171
	v_cvt_pk_fp8_f32 v209, v174, v175
	v_cvt_pk_fp8_f32 v210, v196, v197
	v_cvt_pk_fp8_f32 v211, v200, v201
	v_cvt_pk_fp8_f32 v208, v172, v173 op_sel:[0,0,1]
	v_cvt_pk_fp8_f32 v209, v176, v177 op_sel:[0,0,1]
	v_cvt_pk_fp8_f32 v210, v198, v199 op_sel:[0,0,1]
	v_cvt_pk_fp8_f32 v211, v202, v203 op_sel:[0,0,1]
	s_nop 0
	global_store_dwordx4 v11, v[208:211], s[14:15]
	ds_read_b32 v170, v8
	ds_read_b32 v171, v8 offset:512
	ds_read_b32 v172, v8 offset:1024
	ds_read_b32 v173, v8 offset:1536
	ds_read_b32 v174, v8 offset:2048
	ds_read_b32 v175, v8 offset:2560
	ds_read_b32 v176, v8 offset:3072
	ds_read_b32 v177, v8 offset:3584
	ds_read_b32 v196, v8 offset:4096
	ds_read_b32 v197, v8 offset:4608
	ds_read_b32 v198, v8 offset:5120
	ds_read_b32 v199, v8 offset:5632
	ds_read_b32 v200, v8 offset:6144
	ds_read_b32 v201, v8 offset:6656
	ds_read_b32 v202, v8 offset:7168
	ds_read_b32 v203, v8 offset:7680
	s_waitcnt lgkmcnt(0)
	v_max_f32_e32 v170, v170, v170
	v_max_f32_e32 v171, v171, v171
	v_max_f32_e32 v172, v172, v172
	v_max_f32_e32 v173, v173, v173
	v_max_f32_e32 v174, v174, v174
	v_max_f32_e32 v175, v175, v175
	v_max_f32_e32 v176, v176, v176
	v_max_f32_e32 v177, v177, v177
	v_max_f32_e32 v196, v196, v196
	v_max_f32_e32 v197, v197, v197
	v_max_f32_e32 v198, v198, v198
	v_max_f32_e32 v199, v199, v199
	v_max_f32_e32 v200, v200, v200
	v_max_f32_e32 v201, v201, v201
	v_max_f32_e32 v202, v202, v202
	v_max_f32_e32 v203, v203, v203
	v_med3_f32 v170, v170, s20, v13
	v_med3_f32 v171, v171, s20, v13
	v_med3_f32 v172, v172, s20, v13
	v_med3_f32 v173, v173, s20, v13
	v_med3_f32 v174, v174, s20, v13
	v_med3_f32 v175, v175, s20, v13
	v_med3_f32 v176, v176, s20, v13
	v_med3_f32 v177, v177, s20, v13
	v_med3_f32 v196, v196, s20, v13
	v_med3_f32 v197, v197, s20, v13
	v_med3_f32 v198, v198, s20, v13
	v_med3_f32 v199, v199, s20, v13
	v_med3_f32 v200, v200, s20, v13
	v_med3_f32 v201, v201, s20, v13
	v_med3_f32 v202, v202, s20, v13
	v_med3_f32 v203, v203, s20, v13
	v_mov_b32_e32 v208, 0
	v_mov_b32_e32 v209, 0
	v_mov_b32_e32 v210, 0
	v_mov_b32_e32 v211, 0
	v_cvt_pk_fp8_f32 v208, v170, v171
	v_cvt_pk_fp8_f32 v209, v174, v175
	v_cvt_pk_fp8_f32 v210, v196, v197
	v_cvt_pk_fp8_f32 v211, v200, v201
	v_cvt_pk_fp8_f32 v208, v172, v173 op_sel:[0,0,1]
	v_cvt_pk_fp8_f32 v209, v176, v177 op_sel:[0,0,1]
	v_cvt_pk_fp8_f32 v210, v198, v199 op_sel:[0,0,1]
	v_cvt_pk_fp8_f32 v211, v202, v203 op_sel:[0,0,1]
	s_nop 0
	global_store_dwordx4 v12, v[208:211], s[14:15]
	s_waitcnt vmcnt(32)
	v_mul_f32_e32 v68, 0x43000000, v68
	v_mul_f32_e32 v69, 0x43000000, v69
	v_mul_f32_e32 v70, 0x43000000, v70
	v_mul_f32_e32 v71, 0x43000000, v71
	ds_write_b128 v5, v[68:71]
	v_mul_f32_e32 v72, 0x43000000, v72
	v_mul_f32_e32 v73, 0x43000000, v73
	v_mul_f32_e32 v74, 0x43000000, v74
	v_mul_f32_e32 v75, 0x43000000, v75
	ds_write_b128 v5, v[72:75] offset:1024
	v_mul_f32_e32 v76, 0x43000000, v76
	v_mul_f32_e32 v77, 0x43000000, v77
	v_mul_f32_e32 v78, 0x43000000, v78
	v_mul_f32_e32 v79, 0x43000000, v79
	ds_write_b128 v5, v[76:79] offset:2048
	v_mul_f32_e32 v80, 0x43000000, v80
	v_mul_f32_e32 v81, 0x43000000, v81
	v_mul_f32_e32 v82, 0x43000000, v82
	v_mul_f32_e32 v83, 0x43000000, v83
	ds_write_b128 v5, v[80:83] offset:3072
	v_mul_f32_e32 v84, 0x43000000, v84
	v_mul_f32_e32 v85, 0x43000000, v85
	v_mul_f32_e32 v86, 0x43000000, v86
	v_mul_f32_e32 v87, 0x43000000, v87
	ds_write_b128 v5, v[84:87] offset:4096
	v_mul_f32_e32 v88, 0x43000000, v88
	v_mul_f32_e32 v89, 0x43000000, v89
	v_mul_f32_e32 v90, 0x43000000, v90
	v_mul_f32_e32 v91, 0x43000000, v91
	ds_write_b128 v5, v[88:91] offset:5120
	v_mul_f32_e32 v92, 0x43000000, v92
	v_mul_f32_e32 v93, 0x43000000, v93
	v_mul_f32_e32 v94, 0x43000000, v94
	v_mul_f32_e32 v95, 0x43000000, v95
	ds_write_b128 v5, v[92:95] offset:6144
	v_mul_f32_e32 v96, 0x43000000, v96
	v_mul_f32_e32 v97, 0x43000000, v97
	v_mul_f32_e32 v98, 0x43000000, v98
	v_mul_f32_e32 v99, 0x43000000, v99
	ds_write_b128 v5, v[96:99] offset:7168
	s_waitcnt lgkmcnt(0)
	s_barrier
; #define GAS __attribute__((address_space(1)))
; #define LAS __attribute__((address_space(3)))
; #define LDS_WAIT() asm volatile("s_waitcnt lgkmcnt(0)" ::: "memory")
; __device__ __forceinline__ unsigned pk4_fp8(float a, float b, float c, float d) {
;     a = fminf(fmaxf(a, -448.f), 448.f); b = fminf(fmaxf(b, -448.f), 448.f); c = fminf(fmaxf(c, -448.f), 448.f); d = fminf(fmaxf(d, -448.f), 448.f);
;     int w = __builtin_amdgcn_cvt_pk_fp8_f32(a, b, 0, false); w = __builtin_amdgcn_cvt_pk_fp8_f32(c, d, w, true); return (unsigned)w; }
;     const int pr = item >> 1, kb = 2 * (pr / nblk) + (item & 1), nb = pr % nblk, k0 = 64 * kb, n0 = 32 * nb;
;     const int nr = n0 + (lane & 31); const int sc = MAP == 1 ? src_col_in(nr) : nr;
;     float v[32];
; #pragma unroll
;     for (int i = 0; i < 32; ++i) v[i] = sc >= 0 ? W[(size_t)(k0 + 2 * i + (lane >> 5)) * Nsrc + sc] : 0.f;
; #pragma unroll
;     for (int i = 0; i < 32; ++i) { const int k = k0 + 2 * i + (lane >> 5); float x = v[i] * wscale; if (KS) x *= (k < ksplit ? ksA[k] : ksB[k - ksplit]); scr[(2 * i + (lane >> 5)) * 33 + (lane & 31)] = x; }
;     LDS_WAIT(); asm volatile("" ::: "memory");
;     const int c = lane & 7;
; #pragma unroll
;     for (int j = 0; j < 4; ++j) { const int n = (lane >> 3) + 8 * j; const LAS float* s = scr + (8 * c) * 33 + n;
;         const unsigned long long o = (unsigned long long)pg8::pk4_fp8(s[0 * 33], s[1 * 33], s[2 * 33], s[3 * 33]) | ((unsigned long long)pg8::pk4_fp8(s[4 * 33], s[5 * 33], s[6 * 33], s[7 * 33]) << 32);
;         *(GAS unsigned long long*)(WT + (size_t)(n0 + n) * K + k0 + 8 * c) = o; }
;     LDS_WAIT(); asm volatile("" ::: "memory");
	s_add_i32 s17, s16, 2400
	s_min_u32 s17, s17, 0xfff
	s_lshr_b32 s18, s17, 5
	s_add_i32 s18, s18, 0
	s_and_b32 s19, s17, 31
	s_lshl_b32 s18, s18, 21
	s_lshl_b32 s19, s19, 9
	s_add_u32 s18, s18, s19
	s_add_u32 s12, s2, s18
	s_addc_u32 s13, s3, 0
	global_load_dwordx4 v[68:71], v10, s[12:13]
	s_add_u32 s12, s12, 0x8000
	s_addc_u32 s13, s13, 0
	global_load_dwordx4 v[72:75], v10, s[12:13]
	s_add_u32 s12, s12, 0x8000
	s_addc_u32 s13, s13, 0
	global_load_dwordx4 v[76:79], v10, s[12:13]
	s_add_u32 s12, s12, 0x8000
	s_addc_u32 s13, s13, 0
	global_load_dwordx4 v[80:83], v10, s[12:13]
	s_add_u32 s12, s12, 0x8000
	s_addc_u32 s13, s13, 0
	global_load_dwordx4 v[84:87], v10, s[12:13]
	s_add_u32 s12, s12, 0x8000
	s_addc_u32 s13, s13, 0
	global_load_dwordx4 v[88:91], v10, s[12:13]
	s_add_u32 s12, s12, 0x8000
	s_addc_u32 s13, s13, 0
	global_load_dwordx4 v[92:95], v10, s[12:13]
	s_add_u32 s12, s12, 0x8000
	s_addc_u32 s13, s13, 0
	global_load_dwordx4 v[96:99], v10, s[12:13]
	s_add_i32 s17, s16, 2016
	s_min_u32 s17, s17, 0xfff
	s_lshr_b32 s18, s17, 5
	s_add_i32 s18, s18, 0
	s_and_b32 s19, s17, 31
	s_lshl_b32 s19, s19, 21
	s_lshl_b32 s18, s18, 7
	s_add_u32 s18, s18, s19
	s_add_u32 s14, s4, s18
	s_addc_u32 s15, s5, 0
	ds_read_b32 v170, v7
	ds_read_b32 v171, v7 offset:512
	ds_read_b32 v172, v7 offset:1024
	ds_read_b32 v173, v7 offset:1536
	ds_read_b32 v174, v7 offset:2048
	ds_read_b32 v175, v7 offset:2560
	ds_read_b32 v176, v7 offset:3072
	ds_read_b32 v177, v7 offset:3584
	ds_read_b32 v196, v7 offset:4096
	ds_read_b32 v197, v7 offset:4608
	ds_read_b32 v198, v7 offset:5120
	ds_read_b32 v199, v7 offset:5632
	ds_read_b32 v200, v7 offset:6144
	ds_read_b32 v201, v7 offset:6656
	ds_read_b32 v202, v7 offset:7168
	ds_read_b32 v203, v7 offset:7680
	s_waitcnt lgkmcnt(0)
	v_max_f32_e32 v170, v170, v170
	v_max_f32_e32 v171, v171, v171
	v_max_f32_e32 v172, v172, v172
	v_max_f32_e32 v173, v173, v173
	v_max_f32_e32 v174, v174, v174
	v_max_f32_e32 v175, v175, v175
	v_max_f32_e32 v176, v176, v176
	v_max_f32_e32 v177, v177, v177
	v_max_f32_e32 v196, v196, v196
	v_max_f32_e32 v197, v197, v197
	v_max_f32_e32 v198, v198, v198
	v_max_f32_e32 v199, v199, v199
	v_max_f32_e32 v200, v200, v200
	v_max_f32_e32 v201, v201, v201
	v_max_f32_e32 v202, v202, v202
	v_max_f32_e32 v203, v203, v203
	v_med3_f32 v170, v170, s20, v13
	v_med3_f32 v171, v171, s20, v13
	v_med3_f32 v172, v172, s20, v13
	v_med3_f32 v173, v173, s20, v13
	v_med3_f32 v174, v174, s20, v13
	v_med3_f32 v175, v175, s20, v13
	v_med3_f32 v176, v176, s20, v13
	v_med3_f32 v177, v177, s20, v13
	v_med3_f32 v196, v196, s20, v13
	v_med3_f32 v197, v197, s20, v13
	v_med3_f32 v198, v198, s20, v13
	v_med3_f32 v199, v199, s20, v13
	v_med3_f32 v200, v200, s20, v13
	v_med3_f32 v201, v201, s20, v13
	v_med3_f32 v202, v202, s20, v13
	v_med3_f32 v203, v203, s20, v13
	v_mov_b32_e32 v208, 0
	v_mov_b32_e32 v209, 0
	v_mov_b32_e32 v210, 0
	v_mov_b32_e32 v211, 0
	v_cvt_pk_fp8_f32 v208, v170, v171
	v_cvt_pk_fp8_f32 v209, v174, v175
	v_cvt_pk_fp8_f32 v210, v196, v197
	v_cvt_pk_fp8_f32 v211, v200, v201
	v_cvt_pk_fp8_f32 v208, v172, v173 op_sel:[0,0,1]
	v_cvt_pk_fp8_f32 v209, v176, v177 op_sel:[0,0,1]
	v_cvt_pk_fp8_f32 v210, v198, v199 op_sel:[0,0,1]
	v_cvt_pk_fp8_f32 v211, v202, v203 op_sel:[0,0,1]
	s_nop 0
	global_store_dwordx4 v11, v[208:211], s[14:15]
	ds_read_b32 v170, v9
	ds_read_b32 v171, v9 offset:512
	ds_read_b32 v172, v9 offset:1024
	ds_read_b32 v173, v9 offset:1536
	ds_read_b32 v174, v9 offset:2048
	ds_read_b32 v175, v9 offset:2560
	ds_read_b32 v176, v9 offset:3072
	ds_read_b32 v177, v9 offset:3584
	ds_read_b32 v196, v9 offset:4096
	ds_read_b32 v197, v9 offset:4608
	ds_read_b32 v198, v9 offset:5120
	ds_read_b32 v199, v9 offset:5632
	ds_read_b32 v200, v9 offset:6144
	ds_read_b32 v201, v9 offset:6656
	ds_read_b32 v202, v9 offset:7168
	ds_read_b32 v203, v9 offset:7680
	s_waitcnt lgkmcnt(0)
	v_max_f32_e32 v170, v170, v170
	v_max_f32_e32 v171, v171, v171
	v_max_f32_e32 v172, v172, v172
	v_max_f32_e32 v173, v173, v173
	v_max_f32_e32 v174, v174, v174
	v_max_f32_e32 v175, v175, v175
	v_max_f32_e32 v176, v176, v176
	v_max_f32_e32 v177, v177, v177
	v_max_f32_e32 v196, v196, v196
	v_max_f32_e32 v197, v197, v197
	v_max_f32_e32 v198, v198, v198
	v_max_f32_e32 v199, v199, v199
	v_max_f32_e32 v200, v200, v200
	v_max_f32_e32 v201, v201, v201
	v_max_f32_e32 v202, v202, v202
	v_max_f32_e32 v203, v203, v203
	v_med3_f32 v170, v170, s20, v13
	v_med3_f32 v171, v171, s20, v13
	v_med3_f32 v172, v172, s20, v13
	v_med3_f32 v173, v173, s20, v13
	v_med3_f32 v174, v174, s20, v13
	v_med3_f32 v175, v175, s20, v13
	v_med3_f32 v176, v176, s20, v13
	v_med3_f32 v177, v177, s20, v13
	v_med3_f32 v196, v196, s20, v13
	v_med3_f32 v197, v197, s20, v13
	v_med3_f32 v198, v198, s20, v13
	v_med3_f32 v199, v199, s20, v13
	v_med3_f32 v200, v200, s20, v13
	v_med3_f32 v201, v201, s20, v13
	v_med3_f32 v202, v202, s20, v13
	v_med3_f32 v203, v203, s20, v13
	v_mov_b32_e32 v208, 0
	v_mov_b32_e32 v209, 0
	v_mov_b32_e32 v210, 0
	v_mov_b32_e32 v211, 0
	v_cvt_pk_fp8_f32 v208, v170, v171
	v_cvt_pk_fp8_f32 v209, v174, v175
	v_cvt_pk_fp8_f32 v210, v196, v197
	v_cvt_pk_fp8_f32 v211, v200, v201
	v_cvt_pk_fp8_f32 v208, v172, v173 op_sel:[0,0,1]
	v_cvt_pk_fp8_f32 v209, v176, v177 op_sel:[0,0,1]
	v_cvt_pk_fp8_f32 v210, v198, v199 op_sel:[0,0,1]
	v_cvt_pk_fp8_f32 v211, v202, v203 op_sel:[0,0,1]
	s_nop 0
	global_store_dwordx4 v12, v[208:211], s[14:15]
	s_waitcnt vmcnt(32)
	v_mul_f32_e32 v100, 0x43000000, v100
	v_mul_f32_e32 v101, 0x43000000, v101
	v_mul_f32_e32 v102, 0x43000000, v102
	v_mul_f32_e32 v103, 0x43000000, v103
	ds_write_b128 v4, v[100:103]
	v_mul_f32_e32 v104, 0x43000000, v104
	v_mul_f32_e32 v105, 0x43000000, v105
	v_mul_f32_e32 v106, 0x43000000, v106
	v_mul_f32_e32 v107, 0x43000000, v107
	ds_write_b128 v4, v[104:107] offset:1024
	v_mul_f32_e32 v108, 0x43000000, v108
	v_mul_f32_e32 v109, 0x43000000, v109
	v_mul_f32_e32 v110, 0x43000000, v110
	v_mul_f32_e32 v111, 0x43000000, v111
	ds_write_b128 v4, v[108:111] offset:2048
	v_mul_f32_e32 v112, 0x43000000, v112
	v_mul_f32_e32 v113, 0x43000000, v113
	v_mul_f32_e32 v114, 0x43000000, v114
	v_mul_f32_e32 v115, 0x43000000, v115
	ds_write_b128 v4, v[112:115] offset:3072
	v_mul_f32_e32 v116, 0x43000000, v116
	v_mul_f32_e32 v117, 0x43000000, v117
	v_mul_f32_e32 v118, 0x43000000, v118
	v_mul_f32_e32 v119, 0x43000000, v119
	ds_write_b128 v4, v[116:119] offset:4096
	v_mul_f32_e32 v120, 0x43000000, v120
	v_mul_f32_e32 v121, 0x43000000, v121
	v_mul_f32_e32 v122, 0x43000000, v122
	v_mul_f32_e32 v123, 0x43000000, v123
	ds_write_b128 v4, v[120:123] offset:5120
	v_mul_f32_e32 v124, 0x43000000, v124
	v_mul_f32_e32 v125, 0x43000000, v125
	v_mul_f32_e32 v126, 0x43000000, v126
	v_mul_f32_e32 v127, 0x43000000, v127
	ds_write_b128 v4, v[124:127] offset:6144
	v_mul_f32_e32 v128, 0x43000000, v128
	v_mul_f32_e32 v129, 0x43000000, v129
	v_mul_f32_e32 v130, 0x43000000, v130
	v_mul_f32_e32 v131, 0x43000000, v131
	ds_write_b128 v4, v[128:131] offset:7168
	s_waitcnt lgkmcnt(0)
	s_barrier
; #define GAS __attribute__((address_space(1)))
; #define LAS __attribute__((address_space(3)))
; #define LDS_WAIT() asm volatile("s_waitcnt lgkmcnt(0)" ::: "memory")
; __device__ __forceinline__ unsigned pk4_fp8(float a, float b, float c, float d) {
;     a = fminf(fmaxf(a, -448.f), 448.f); b = fminf(fmaxf(b, -448.f), 448.f); c = fminf(fmaxf(c, -448.f), 448.f); d = fminf(fmaxf(d, -448.f), 448.f);
;     int w = __builtin_amdgcn_cvt_pk_fp8_f32(a, b, 0, false); w = __builtin_amdgcn_cvt_pk_fp8_f32(c, d, w, true); return (unsigned)w; }
;     const int pr = item >> 1, kb = 2 * (pr / nblk) + (item & 1), nb = pr % nblk, k0 = 64 * kb, n0 = 32 * nb;
;     const int nr = n0 + (lane & 31); const int sc = MAP == 1 ? src_col_in(nr) : nr;
;     float v[32];
; #pragma unroll
;     for (int i = 0; i < 32; ++i) v[i] = sc >= 0 ? W[(size_t)(k0 + 2 * i + (lane >> 5)) * Nsrc + sc] : 0.f;
; #pragma unroll
;     for (int i = 0; i < 32; ++i) { const int k = k0 + 2 * i + (lane >> 5); float x = v[i] * wscale; if (KS) x *= (k < ksplit ? ksA[k] : ksB[k - ksplit]); scr[(2 * i + (lane >> 5)) * 33 + (lane & 31)] = x; }
;     LDS_WAIT(); asm volatile("" ::: "memory");
;     const int c = lane & 7;
; #pragma unroll
;     for (int j = 0; j < 4; ++j) { const int n = (lane >> 3) + 8 * j; const LAS float* s = scr + (8 * c) * 33 + n;
;         const unsigned long long o = (unsigned long long)pg8::pk4_fp8(s[0 * 33], s[1 * 33], s[2 * 33], s[3 * 33]) | ((unsigned long long)pg8::pk4_fp8(s[4 * 33], s[5 * 33], s[6 * 33], s[7 * 33]) << 32);
;         *(GAS unsigned long long*)(WT + (size_t)(n0 + n) * K + k0 + 8 * c) = o; }
;     LDS_WAIT(); asm volatile("" ::: "memory");
	s_add_i32 s17, s16, 2496
	s_min_u32 s17, s17, 0xfff
	s_lshr_b32 s18, s17, 5
	s_add_i32 s18, s18, 0
	s_and_b32 s19, s17, 31
	s_lshl_b32 s18, s18, 21
	s_lshl_b32 s19, s19, 9
	s_add_u32 s18, s18, s19
	s_add_u32 s12, s2, s18
	s_addc_u32 s13, s3, 0
	global_load_dwordx4 v[100:103], v10, s[12:13]
	s_add_u32 s12, s12, 0x8000
	s_addc_u32 s13, s13, 0
	global_load_dwordx4 v[104:107], v10, s[12:13]
	s_add_u32 s12, s12, 0x8000
	s_addc_u32 s13, s13, 0
	global_load_dwordx4 v[108:111], v10, s[12:13]
	s_add_u32 s12, s12, 0x8000
	s_addc_u32 s13, s13, 0
	global_load_dwordx4 v[112:115], v10, s[12:13]
	s_add_u32 s12, s12, 0x8000
	s_addc_u32 s13, s13, 0
	global_load_dwordx4 v[116:119], v10, s[12:13]
	s_add_u32 s12, s12, 0x8000
	s_addc_u32 s13, s13, 0
	global_load_dwordx4 v[120:123], v10, s[12:13]
	s_add_u32 s12, s12, 0x8000
	s_addc_u32 s13, s13, 0
	global_load_dwordx4 v[124:127], v10, s[12:13]
	s_add_u32 s12, s12, 0x8000
	s_addc_u32 s13, s13, 0
	global_load_dwordx4 v[128:131], v10, s[12:13]
	s_add_i32 s17, s16, 2112
	s_min_u32 s17, s17, 0xfff
	s_lshr_b32 s18, s17, 5
	s_add_i32 s18, s18, 0
	s_and_b32 s19, s17, 31
	s_lshl_b32 s19, s19, 21
	s_lshl_b32 s18, s18, 7
	s_add_u32 s18, s18, s19
	s_add_u32 s14, s4, s18
	s_addc_u32 s15, s5, 0
	ds_read_b32 v170, v6
	ds_read_b32 v171, v6 offset:512
	ds_read_b32 v172, v6 offset:1024
	ds_read_b32 v173, v6 offset:1536
	ds_read_b32 v174, v6 offset:2048
	ds_read_b32 v175, v6 offset:2560
	ds_read_b32 v176, v6 offset:3072
	ds_read_b32 v177, v6 offset:3584
	ds_read_b32 v196, v6 offset:4096
	ds_read_b32 v197, v6 offset:4608
	ds_read_b32 v198, v6 offset:5120
	ds_read_b32 v199, v6 offset:5632
	ds_read_b32 v200, v6 offset:6144
	ds_read_b32 v201, v6 offset:6656
	ds_read_b32 v202, v6 offset:7168
	ds_read_b32 v203, v6 offset:7680
	s_waitcnt lgkmcnt(0)
	v_max_f32_e32 v170, v170, v170
	v_max_f32_e32 v171, v171, v171
	v_max_f32_e32 v172, v172, v172
	v_max_f32_e32 v173, v173, v173
	v_max_f32_e32 v174, v174, v174
	v_max_f32_e32 v175, v175, v175
	v_max_f32_e32 v176, v176, v176
	v_max_f32_e32 v177, v177, v177
	v_max_f32_e32 v196, v196, v196
	v_max_f32_e32 v197, v197, v197
	v_max_f32_e32 v198, v198, v198
	v_max_f32_e32 v199, v199, v199
	v_max_f32_e32 v200, v200, v200
	v_max_f32_e32 v201, v201, v201
	v_max_f32_e32 v202, v202, v202
	v_max_f32_e32 v203, v203, v203
	v_med3_f32 v170, v170, s20, v13
	v_med3_f32 v171, v171, s20, v13
	v_med3_f32 v172, v172, s20, v13
	v_med3_f32 v173, v173, s20, v13
	v_med3_f32 v174, v174, s20, v13
	v_med3_f32 v175, v175, s20, v13
	v_med3_f32 v176, v176, s20, v13
	v_med3_f32 v177, v177, s20, v13
	v_med3_f32 v196, v196, s20, v13
	v_med3_f32 v197, v197, s20, v13
	v_med3_f32 v198, v198, s20, v13
	v_med3_f32 v199, v199, s20, v13
	v_med3_f32 v200, v200, s20, v13
	v_med3_f32 v201, v201, s20, v13
	v_med3_f32 v202, v202, s20, v13
	v_med3_f32 v203, v203, s20, v13
	v_mov_b32_e32 v208, 0
	v_mov_b32_e32 v209, 0
	v_mov_b32_e32 v210, 0
	v_mov_b32_e32 v211, 0
	v_cvt_pk_fp8_f32 v208, v170, v171
	v_cvt_pk_fp8_f32 v209, v174, v175
	v_cvt_pk_fp8_f32 v210, v196, v197
	v_cvt_pk_fp8_f32 v211, v200, v201
	v_cvt_pk_fp8_f32 v208, v172, v173 op_sel:[0,0,1]
	v_cvt_pk_fp8_f32 v209, v176, v177 op_sel:[0,0,1]
	v_cvt_pk_fp8_f32 v210, v198, v199 op_sel:[0,0,1]
	v_cvt_pk_fp8_f32 v211, v202, v203 op_sel:[0,0,1]
	s_nop 0
	global_store_dwordx4 v11, v[208:211], s[14:15]
	ds_read_b32 v170, v8
	ds_read_b32 v171, v8 offset:512
	ds_read_b32 v172, v8 offset:1024
	ds_read_b32 v173, v8 offset:1536
	ds_read_b32 v174, v8 offset:2048
	ds_read_b32 v175, v8 offset:2560
	ds_read_b32 v176, v8 offset:3072
	ds_read_b32 v177, v8 offset:3584
	ds_read_b32 v196, v8 offset:4096
	ds_read_b32 v197, v8 offset:4608
	ds_read_b32 v198, v8 offset:5120
	ds_read_b32 v199, v8 offset:5632
	ds_read_b32 v200, v8 offset:6144
	ds_read_b32 v201, v8 offset:6656
	ds_read_b32 v202, v8 offset:7168
	ds_read_b32 v203, v8 offset:7680
	s_waitcnt lgkmcnt(0)
	v_max_f32_e32 v170, v170, v170
	v_max_f32_e32 v171, v171, v171
	v_max_f32_e32 v172, v172, v172
	v_max_f32_e32 v173, v173, v173
	v_max_f32_e32 v174, v174, v174
	v_max_f32_e32 v175, v175, v175
	v_max_f32_e32 v176, v176, v176
	v_max_f32_e32 v177, v177, v177
	v_max_f32_e32 v196, v196, v196
	v_max_f32_e32 v197, v197, v197
	v_max_f32_e32 v198, v198, v198
	v_max_f32_e32 v199, v199, v199
	v_max_f32_e32 v200, v200, v200
	v_max_f32_e32 v201, v201, v201
	v_max_f32_e32 v202, v202, v202
	v_max_f32_e32 v203, v203, v203
	v_med3_f32 v170, v170, s20, v13
	v_med3_f32 v171, v171, s20, v13
	v_med3_f32 v172, v172, s20, v13
	v_med3_f32 v173, v173, s20, v13
	v_med3_f32 v174, v174, s20, v13
	v_med3_f32 v175, v175, s20, v13
	v_med3_f32 v176, v176, s20, v13
	v_med3_f32 v177, v177, s20, v13
	v_med3_f32 v196, v196, s20, v13
	v_med3_f32 v197, v197, s20, v13
	v_med3_f32 v198, v198, s20, v13
	v_med3_f32 v199, v199, s20, v13
	v_med3_f32 v200, v200, s20, v13
	v_med3_f32 v201, v201, s20, v13
	v_med3_f32 v202, v202, s20, v13
	v_med3_f32 v203, v203, s20, v13
	v_mov_b32_e32 v208, 0
	v_mov_b32_e32 v209, 0
	v_mov_b32_e32 v210, 0
	v_mov_b32_e32 v211, 0
	v_cvt_pk_fp8_f32 v208, v170, v171
	v_cvt_pk_fp8_f32 v209, v174, v175
	v_cvt_pk_fp8_f32 v210, v196, v197
	v_cvt_pk_fp8_f32 v211, v200, v201
	v_cvt_pk_fp8_f32 v208, v172, v173 op_sel:[0,0,1]
	v_cvt_pk_fp8_f32 v209, v176, v177 op_sel:[0,0,1]
	v_cvt_pk_fp8_f32 v210, v198, v199 op_sel:[0,0,1]
	v_cvt_pk_fp8_f32 v211, v202, v203 op_sel:[0,0,1]
	s_nop 0
	global_store_dwordx4 v12, v[208:211], s[14:15]
	s_waitcnt vmcnt(32)
	v_mul_f32_e32 v132, 0x43000000, v132
	v_mul_f32_e32 v133, 0x43000000, v133
	v_mul_f32_e32 v134, 0x43000000, v134
	v_mul_f32_e32 v135, 0x43000000, v135
	ds_write_b128 v5, v[132:135]
	v_mul_f32_e32 v136, 0x43000000, v136
	v_mul_f32_e32 v137, 0x43000000, v137
	v_mul_f32_e32 v138, 0x43000000, v138
	v_mul_f32_e32 v139, 0x43000000, v139
	ds_write_b128 v5, v[136:139] offset:1024
	v_mul_f32_e32 v140, 0x43000000, v140
	v_mul_f32_e32 v141, 0x43000000, v141
	v_mul_f32_e32 v142, 0x43000000, v142
	v_mul_f32_e32 v143, 0x43000000, v143
	ds_write_b128 v5, v[140:143] offset:2048
	v_mul_f32_e32 v144, 0x43000000, v144
	v_mul_f32_e32 v145, 0x43000000, v145
	v_mul_f32_e32 v146, 0x43000000, v146
	v_mul_f32_e32 v147, 0x43000000, v147
	ds_write_b128 v5, v[144:147] offset:3072
	v_mul_f32_e32 v148, 0x43000000, v148
	v_mul_f32_e32 v149, 0x43000000, v149
	v_mul_f32_e32 v150, 0x43000000, v150
	v_mul_f32_e32 v151, 0x43000000, v151
	ds_write_b128 v5, v[148:151] offset:4096
	v_mul_f32_e32 v152, 0x43000000, v152
	v_mul_f32_e32 v153, 0x43000000, v153
	v_mul_f32_e32 v154, 0x43000000, v154
	v_mul_f32_e32 v155, 0x43000000, v155
	ds_write_b128 v5, v[152:155] offset:5120
	v_mul_f32_e32 v156, 0x43000000, v156
	v_mul_f32_e32 v157, 0x43000000, v157
	v_mul_f32_e32 v158, 0x43000000, v158
	v_mul_f32_e32 v159, 0x43000000, v159
	ds_write_b128 v5, v[156:159] offset:6144
	v_mul_f32_e32 v160, 0x43000000, v160
	v_mul_f32_e32 v161, 0x43000000, v161
	v_mul_f32_e32 v162, 0x43000000, v162
	v_mul_f32_e32 v163, 0x43000000, v163
	ds_write_b128 v5, v[160:163] offset:7168
	s_waitcnt lgkmcnt(0)
	s_barrier
; #define GAS __attribute__((address_space(1)))
; #define LAS __attribute__((address_space(3)))
; #define LDS_WAIT() asm volatile("s_waitcnt lgkmcnt(0)" ::: "memory")
;     const int pr = item >> 1, kb = 2 * (pr / nblk) + (item & 1), nb = pr % nblk, k0 = 64 * kb, n0 = 32 * nb;
;     const int nr = n0 + (lane & 31); const int sc = MAP == 1 ? src_col_in(nr) : nr;
;     float v[32];
; #pragma unroll
;     for (int i = 0; i < 32; ++i) v[i] = sc >= 0 ? W[(size_t)(k0 + 2 * i + (lane >> 5)) * Nsrc + sc] : 0.f;
; #pragma unroll
;     for (int i = 0; i < 32; ++i) { const int k = k0 + 2 * i + (lane >> 5); float x = v[i] * wscale; if (KS) x *= (k < ksplit ? ksA[k] : ksB[k - ksplit]); scr[(2 * i + (lane >> 5)) * 33 + (lane & 31)] = x; }
;     LDS_WAIT(); asm volatile("" ::: "memory");
;     const int c = lane & 7;
; #pragma unroll
;     for (int j = 0; j < 4; ++j) { const int n = (lane >> 3) + 8 * j; const LAS float* s = scr + (8 * c) * 33 + n;
;         const unsigned long long o = (unsigned long long)pg8::pk4_fp8(s[0 * 33], s[1 * 33], s[2 * 33], s[3 * 33]) | ((unsigned long long)pg8::pk4_fp8(s[4 * 33], s[5 * 33], s[6 * 33], s[7 * 33]) << 32);
;         *(GAS unsigned long long*)(WT + (size_t)(n0 + n) * K + k0 + 8 * c) = o; }
;     LDS_WAIT(); asm volatile("" ::: "memory");
; }
; __global__ void __launch_bounds__(NWAVES * 64, 2) hybrid_fwd(Args args) {
;     ...
;             p0_transpose_item_f8<false>(args.in[16] + (size_t)l * FF * DM, FF, DM, DM / 32, (unsigned char*)(ws + WS_WDN + l * SZ_WDN), 128.f, args.in[16], args.in[16], 0, scr, r, lane);
	s_add_i32 s17, s16, 2592
	s_min_u32 s17, s17, 0xfff
	s_lshr_b32 s18, s17, 5
	s_add_i32 s18, s18, 0
	s_and_b32 s19, s17, 31
	s_lshl_b32 s18, s18, 21
	s_lshl_b32 s19, s19, 9
	s_add_u32 s18, s18, s19
	s_add_u32 s12, s2, s18
	s_addc_u32 s13, s3, 0
	global_load_dwordx4 v[132:135], v10, s[12:13]
	s_add_u32 s12, s12, 0x8000
	s_addc_u32 s13, s13, 0
	global_load_dwordx4 v[136:139], v10, s[12:13]
	s_add_u32 s12, s12, 0x8000
	s_addc_u32 s13, s13, 0
	global_load_dwordx4 v[140:143], v10, s[12:13]
	s_add_u32 s12, s12, 0x8000
	s_addc_u32 s13, s13, 0
	global_load_dwordx4 v[144:147], v10, s[12:13]
	s_add_u32 s12, s12, 0x8000
	s_addc_u32 s13, s13, 0
	global_load_dwordx4 v[148:151], v10, s[12:13]
	s_add_u32 s12, s12, 0x8000
	s_addc_u32 s13, s13, 0
	global_load_dwordx4 v[152:155], v10, s[12:13]
	s_add_u32 s12, s12, 0x8000
	s_addc_u32 s13, s13, 0
	global_load_dwordx4 v[156:159], v10, s[12:13]
	s_add_u32 s12, s12, 0x8000
	s_addc_u32 s13, s13, 0
	global_load_dwordx4 v[160:163], v10, s[12:13]
	s_add_i32 s17, s16, 2208
	s_min_u32 s17, s17, 0xfff
	s_lshr_b32 s18, s17, 5
	s_add_i32 s18, s18, 0
	s_and_b32 s19, s17, 31
	s_lshl_b32 s19, s19, 21
	s_lshl_b32 s18, s18, 7
	s_add_u32 s18, s18, s19
	s_add_u32 s14, s4, s18
	s_addc_u32 s15, s5, 0
	ds_read_b32 v170, v7
	ds_read_b32 v171, v7 offset:512
	ds_read_b32 v172, v7 offset:1024
	ds_read_b32 v173, v7 offset:1536
	ds_read_b32 v174, v7 offset:2048
	ds_read_b32 v175, v7 offset:2560
	ds_read_b32 v176, v7 offset:3072
	ds_read_b32 v177, v7 offset:3584
	ds_read_b32 v196, v7 offset:4096
	ds_read_b32 v197, v7 offset:4608
	ds_read_b32 v198, v7 offset:5120
	ds_read_b32 v199, v7 offset:5632
	ds_read_b32 v200, v7 offset:6144
	ds_read_b32 v201, v7 offset:6656
	ds_read_b32 v202, v7 offset:7168
	ds_read_b32 v203, v7 offset:7680
	s_waitcnt lgkmcnt(0)
	v_max_f32_e32 v170, v170, v170
	v_max_f32_e32 v171, v171, v171
	v_max_f32_e32 v172, v172, v172
	v_max_f32_e32 v173, v173, v173
	v_max_f32_e32 v174, v174, v174
	v_max_f32_e32 v175, v175, v175
	v_max_f32_e32 v176, v176, v176
	v_max_f32_e32 v177, v177, v177
	v_max_f32_e32 v196, v196, v196
	v_max_f32_e32 v197, v197, v197
	v_max_f32_e32 v198, v198, v198
	v_max_f32_e32 v199, v199, v199
	v_max_f32_e32 v200, v200, v200
	v_max_f32_e32 v201, v201, v201
	v_max_f32_e32 v202, v202, v202
	v_max_f32_e32 v203, v203, v203
	v_med3_f32 v170, v170, s20, v13
	v_med3_f32 v171, v171, s20, v13
	v_med3_f32 v172, v172, s20, v13
	v_med3_f32 v173, v173, s20, v13
	v_med3_f32 v174, v174, s20, v13
	v_med3_f32 v175, v175, s20, v13
	v_med3_f32 v176, v176, s20, v13
	v_med3_f32 v177, v177, s20, v13
	v_med3_f32 v196, v196, s20, v13
	v_med3_f32 v197, v197, s20, v13
	v_med3_f32 v198, v198, s20, v13
	v_med3_f32 v199, v199, s20, v13
	v_med3_f32 v200, v200, s20, v13
	v_med3_f32 v201, v201, s20, v13
	v_med3_f32 v202, v202, s20, v13
	v_med3_f32 v203, v203, s20, v13
	v_mov_b32_e32 v208, 0
	v_mov_b32_e32 v209, 0
	v_mov_b32_e32 v210, 0
	v_mov_b32_e32 v211, 0
	v_cvt_pk_fp8_f32 v208, v170, v171
	v_cvt_pk_fp8_f32 v209, v174, v175
	v_cvt_pk_fp8_f32 v210, v196, v197
	v_cvt_pk_fp8_f32 v211, v200, v201
	v_cvt_pk_fp8_f32 v208, v172, v173 op_sel:[0,0,1]
	v_cvt_pk_fp8_f32 v209, v176, v177 op_sel:[0,0,1]
	v_cvt_pk_fp8_f32 v210, v198, v199 op_sel:[0,0,1]
	v_cvt_pk_fp8_f32 v211, v202, v203 op_sel:[0,0,1]
	s_nop 0
	global_store_dwordx4 v11, v[208:211], s[14:15]
	ds_read_b32 v170, v9
	ds_read_b32 v171, v9 offset:512
	ds_read_b32 v172, v9 offset:1024
	ds_read_b32 v173, v9 offset:1536
	ds_read_b32 v174, v9 offset:2048
	ds_read_b32 v175, v9 offset:2560
	ds_read_b32 v176, v9 offset:3072
	ds_read_b32 v177, v9 offset:3584
	ds_read_b32 v196, v9 offset:4096
	ds_read_b32 v197, v9 offset:4608
	ds_read_b32 v198, v9 offset:5120
	ds_read_b32 v199, v9 offset:5632
	ds_read_b32 v200, v9 offset:6144
	ds_read_b32 v201, v9 offset:6656
	ds_read_b32 v202, v9 offset:7168
	ds_read_b32 v203, v9 offset:7680
	s_waitcnt lgkmcnt(0)
	v_max_f32_e32 v170, v170, v170
	v_max_f32_e32 v171, v171, v171
	v_max_f32_e32 v172, v172, v172
	v_max_f32_e32 v173, v173, v173
	v_max_f32_e32 v174, v174, v174
	v_max_f32_e32 v175, v175, v175
	v_max_f32_e32 v176, v176, v176
	v_max_f32_e32 v177, v177, v177
	v_max_f32_e32 v196, v196, v196
	v_max_f32_e32 v197, v197, v197
	v_max_f32_e32 v198, v198, v198
	v_max_f32_e32 v199, v199, v199
	v_max_f32_e32 v200, v200, v200
	v_max_f32_e32 v201, v201, v201
	v_max_f32_e32 v202, v202, v202
	v_max_f32_e32 v203, v203, v203
	v_med3_f32 v170, v170, s20, v13
	v_med3_f32 v171, v171, s20, v13
	v_med3_f32 v172, v172, s20, v13
	v_med3_f32 v173, v173, s20, v13
	v_med3_f32 v174, v174, s20, v13
	v_med3_f32 v175, v175, s20, v13
	v_med3_f32 v176, v176, s20, v13
	v_med3_f32 v177, v177, s20, v13
	v_med3_f32 v196, v196, s20, v13
	v_med3_f32 v197, v197, s20, v13
	v_med3_f32 v198, v198, s20, v13
	v_med3_f32 v199, v199, s20, v13
	v_med3_f32 v200, v200, s20, v13
	v_med3_f32 v201, v201, s20, v13
	v_med3_f32 v202, v202, s20, v13
	v_med3_f32 v203, v203, s20, v13
	v_mov_b32_e32 v208, 0
	v_mov_b32_e32 v209, 0
	v_mov_b32_e32 v210, 0
	v_mov_b32_e32 v211, 0
	v_cvt_pk_fp8_f32 v208, v170, v171
	v_cvt_pk_fp8_f32 v209, v174, v175
	v_cvt_pk_fp8_f32 v210, v196, v197
	v_cvt_pk_fp8_f32 v211, v200, v201
	v_cvt_pk_fp8_f32 v208, v172, v173 op_sel:[0,0,1]
	v_cvt_pk_fp8_f32 v209, v176, v177 op_sel:[0,0,1]
	v_cvt_pk_fp8_f32 v210, v198, v199 op_sel:[0,0,1]
	v_cvt_pk_fp8_f32 v211, v202, v203 op_sel:[0,0,1]
	s_nop 0
	global_store_dwordx4 v12, v[208:211], s[14:15]
	s_waitcnt vmcnt(32)
	v_mul_f32_e32 v36, 0x43000000, v36
	v_mul_f32_e32 v37, 0x43000000, v37
	v_mul_f32_e32 v38, 0x43000000, v38
	v_mul_f32_e32 v39, 0x43000000, v39
	ds_write_b128 v4, v[36:39]
	v_mul_f32_e32 v40, 0x43000000, v40
	v_mul_f32_e32 v41, 0x43000000, v41
	v_mul_f32_e32 v42, 0x43000000, v42
	v_mul_f32_e32 v43, 0x43000000, v43
	ds_write_b128 v4, v[40:43] offset:1024
	v_mul_f32_e32 v44, 0x43000000, v44
	v_mul_f32_e32 v45, 0x43000000, v45
	v_mul_f32_e32 v46, 0x43000000, v46
	v_mul_f32_e32 v47, 0x43000000, v47
	ds_write_b128 v4, v[44:47] offset:2048
	v_mul_f32_e32 v48, 0x43000000, v48
	v_mul_f32_e32 v49, 0x43000000, v49
	v_mul_f32_e32 v50, 0x43000000, v50
	v_mul_f32_e32 v51, 0x43000000, v51
	ds_write_b128 v4, v[48:51] offset:3072
	v_mul_f32_e32 v52, 0x43000000, v52
	v_mul_f32_e32 v53, 0x43000000, v53
	v_mul_f32_e32 v54, 0x43000000, v54
	v_mul_f32_e32 v55, 0x43000000, v55
	ds_write_b128 v4, v[52:55] offset:4096
	v_mul_f32_e32 v56, 0x43000000, v56
	v_mul_f32_e32 v57, 0x43000000, v57
	v_mul_f32_e32 v58, 0x43000000, v58
	v_mul_f32_e32 v59, 0x43000000, v59
	ds_write_b128 v4, v[56:59] offset:5120
	v_mul_f32_e32 v60, 0x43000000, v60
	v_mul_f32_e32 v61, 0x43000000, v61
	v_mul_f32_e32 v62, 0x43000000, v62
	v_mul_f32_e32 v63, 0x43000000, v63
	ds_write_b128 v4, v[60:63] offset:6144
	v_mul_f32_e32 v64, 0x43000000, v64
	v_mul_f32_e32 v65, 0x43000000, v65
	v_mul_f32_e32 v66, 0x43000000, v66
	v_mul_f32_e32 v67, 0x43000000, v67
	ds_write_b128 v4, v[64:67] offset:7168
	s_waitcnt lgkmcnt(0)
	s_barrier
; #define GAS __attribute__((address_space(1)))
; #define LAS __attribute__((address_space(3)))
; #define LDS_WAIT() asm volatile("s_waitcnt lgkmcnt(0)" ::: "memory")
;     const int pr = item >> 1, kb = 2 * (pr / nblk) + (item & 1), nb = pr % nblk, k0 = 64 * kb, n0 = 32 * nb;
;     const int nr = n0 + (lane & 31); const int sc = MAP == 1 ? src_col_in(nr) : nr;
;     float v[32];
; #pragma unroll
;     for (int i = 0; i < 32; ++i) v[i] = sc >= 0 ? W[(size_t)(k0 + 2 * i + (lane >> 5)) * Nsrc + sc] : 0.f;
; #pragma unroll
;     for (int i = 0; i < 32; ++i) { const int k = k0 + 2 * i + (lane >> 5); float x = v[i] * wscale; if (KS) x *= (k < ksplit ? ksA[k] : ksB[k - ksplit]); scr[(2 * i + (lane >> 5)) * 33 + (lane & 31)] = x; }
;     LDS_WAIT(); asm volatile("" ::: "memory");
;     const int c = lane & 7;
; #pragma unroll
;     for (int j = 0; j < 4; ++j) { const int n = (lane >> 3) + 8 * j; const LAS float* s = scr + (8 * c) * 33 + n;
;         const unsigned long long o = (unsigned long long)pg8::pk4_fp8(s[0 * 33], s[1 * 33], s[2 * 33], s[3 * 33]) | ((unsigned long long)pg8::pk4_fp8(s[4 * 33], s[5 * 33], s[6 * 33], s[7 * 33]) << 32);
;         *(GAS unsigned long long*)(WT + (size_t)(n0 + n) * K + k0 + 8 * c) = o; }
;     LDS_WAIT(); asm volatile("" ::: "memory");
; }
; __global__ void __launch_bounds__(NWAVES * 64, 2) hybrid_fwd(Args args) {
;     ...
;             p0_transpose_item_f8<false>(args.in[16] + (size_t)l * FF * DM, FF, DM, DM / 32, (unsigned char*)(ws + WS_WDN + l * SZ_WDN), 128.f, args.in[16], args.in[16], 0, scr, r, lane);
	s_add_i32 s17, s16, 2688
	s_min_u32 s17, s17, 0xfff
	s_lshr_b32 s18, s17, 5
	s_add_i32 s18, s18, 0
	s_and_b32 s19, s17, 31
	s_lshl_b32 s18, s18, 21
	s_lshl_b32 s19, s19, 9
	s_add_u32 s18, s18, s19
	s_add_u32 s12, s2, s18
	s_addc_u32 s13, s3, 0
	global_load_dwordx4 v[36:39], v10, s[12:13]
	s_add_u32 s12, s12, 0x8000
	s_addc_u32 s13, s13, 0
	global_load_dwordx4 v[40:43], v10, s[12:13]
	s_add_u32 s12, s12, 0x8000
	s_addc_u32 s13, s13, 0
	global_load_dwordx4 v[44:47], v10, s[12:13]
	s_add_u32 s12, s12, 0x8000
	s_addc_u32 s13, s13, 0
	global_load_dwordx4 v[48:51], v10, s[12:13]
	s_add_u32 s12, s12, 0x8000
	s_addc_u32 s13, s13, 0
	global_load_dwordx4 v[52:55], v10, s[12:13]
	s_add_u32 s12, s12, 0x8000
	s_addc_u32 s13, s13, 0
	global_load_dwordx4 v[56:59], v10, s[12:13]
	s_add_u32 s12, s12, 0x8000
	s_addc_u32 s13, s13, 0
	global_load_dwordx4 v[60:63], v10, s[12:13]
	s_add_u32 s12, s12, 0x8000
	s_addc_u32 s13, s13, 0
	global_load_dwordx4 v[64:67], v10, s[12:13]
	s_add_i32 s17, s16, 2304
	s_min_u32 s17, s17, 0xfff
	s_lshr_b32 s18, s17, 5
	s_add_i32 s18, s18, 0
	s_and_b32 s19, s17, 31
	s_lshl_b32 s19, s19, 21
	s_lshl_b32 s18, s18, 7
	s_add_u32 s18, s18, s19
	s_add_u32 s14, s4, s18
	s_addc_u32 s15, s5, 0
	ds_read_b32 v170, v6
	ds_read_b32 v171, v6 offset:512
	ds_read_b32 v172, v6 offset:1024
	ds_read_b32 v173, v6 offset:1536
	ds_read_b32 v174, v6 offset:2048
	ds_read_b32 v175, v6 offset:2560
	ds_read_b32 v176, v6 offset:3072
	ds_read_b32 v177, v6 offset:3584
	ds_read_b32 v196, v6 offset:4096
	ds_read_b32 v197, v6 offset:4608
	ds_read_b32 v198, v6 offset:5120
	ds_read_b32 v199, v6 offset:5632
	ds_read_b32 v200, v6 offset:6144
	ds_read_b32 v201, v6 offset:6656
	ds_read_b32 v202, v6 offset:7168
	ds_read_b32 v203, v6 offset:7680
	s_waitcnt lgkmcnt(0)
	v_max_f32_e32 v170, v170, v170
	v_max_f32_e32 v171, v171, v171
	v_max_f32_e32 v172, v172, v172
	v_max_f32_e32 v173, v173, v173
	v_max_f32_e32 v174, v174, v174
	v_max_f32_e32 v175, v175, v175
	v_max_f32_e32 v176, v176, v176
	v_max_f32_e32 v177, v177, v177
	v_max_f32_e32 v196, v196, v196
	v_max_f32_e32 v197, v197, v197
	v_max_f32_e32 v198, v198, v198
	v_max_f32_e32 v199, v199, v199
	v_max_f32_e32 v200, v200, v200
	v_max_f32_e32 v201, v201, v201
	v_max_f32_e32 v202, v202, v202
	v_max_f32_e32 v203, v203, v203
	v_med3_f32 v170, v170, s20, v13
	v_med3_f32 v171, v171, s20, v13
	v_med3_f32 v172, v172, s20, v13
	v_med3_f32 v173, v173, s20, v13
	v_med3_f32 v174, v174, s20, v13
	v_med3_f32 v175, v175, s20, v13
	v_med3_f32 v176, v176, s20, v13
	v_med3_f32 v177, v177, s20, v13
	v_med3_f32 v196, v196, s20, v13
	v_med3_f32 v197, v197, s20, v13
	v_med3_f32 v198, v198, s20, v13
	v_med3_f32 v199, v199, s20, v13
	v_med3_f32 v200, v200, s20, v13
	v_med3_f32 v201, v201, s20, v13
	v_med3_f32 v202, v202, s20, v13
	v_med3_f32 v203, v203, s20, v13
	v_mov_b32_e32 v208, 0
	v_mov_b32_e32 v209, 0
	v_mov_b32_e32 v210, 0
	v_mov_b32_e32 v211, 0
	v_cvt_pk_fp8_f32 v208, v170, v171
	v_cvt_pk_fp8_f32 v209, v174, v175
	v_cvt_pk_fp8_f32 v210, v196, v197
	v_cvt_pk_fp8_f32 v211, v200, v201
	v_cvt_pk_fp8_f32 v208, v172, v173 op_sel:[0,0,1]
	v_cvt_pk_fp8_f32 v209, v176, v177 op_sel:[0,0,1]
	v_cvt_pk_fp8_f32 v210, v198, v199 op_sel:[0,0,1]
	v_cvt_pk_fp8_f32 v211, v202, v203 op_sel:[0,0,1]
	s_nop 0
	global_store_dwordx4 v11, v[208:211], s[14:15]
	ds_read_b32 v170, v8
	ds_read_b32 v171, v8 offset:512
	ds_read_b32 v172, v8 offset:1024
	ds_read_b32 v173, v8 offset:1536
	ds_read_b32 v174, v8 offset:2048
	ds_read_b32 v175, v8 offset:2560
	ds_read_b32 v176, v8 offset:3072
	ds_read_b32 v177, v8 offset:3584
	ds_read_b32 v196, v8 offset:4096
	ds_read_b32 v197, v8 offset:4608
	ds_read_b32 v198, v8 offset:5120
	ds_read_b32 v199, v8 offset:5632
	ds_read_b32 v200, v8 offset:6144
	ds_read_b32 v201, v8 offset:6656
	ds_read_b32 v202, v8 offset:7168
	ds_read_b32 v203, v8 offset:7680
	s_waitcnt lgkmcnt(0)
	v_max_f32_e32 v170, v170, v170
	v_max_f32_e32 v171, v171, v171
	v_max_f32_e32 v172, v172, v172
	v_max_f32_e32 v173, v173, v173
	v_max_f32_e32 v174, v174, v174
	v_max_f32_e32 v175, v175, v175
	v_max_f32_e32 v176, v176, v176
	v_max_f32_e32 v177, v177, v177
	v_max_f32_e32 v196, v196, v196
	v_max_f32_e32 v197, v197, v197
	v_max_f32_e32 v198, v198, v198
	v_max_f32_e32 v199, v199, v199
	v_max_f32_e32 v200, v200, v200
	v_max_f32_e32 v201, v201, v201
	v_max_f32_e32 v202, v202, v202
	v_max_f32_e32 v203, v203, v203
	v_med3_f32 v170, v170, s20, v13
	v_med3_f32 v171, v171, s20, v13
	v_med3_f32 v172, v172, s20, v13
	v_med3_f32 v173, v173, s20, v13
	v_med3_f32 v174, v174, s20, v13
	v_med3_f32 v175, v175, s20, v13
	v_med3_f32 v176, v176, s20, v13
	v_med3_f32 v177, v177, s20, v13
	v_med3_f32 v196, v196, s20, v13
	v_med3_f32 v197, v197, s20, v13
	v_med3_f32 v198, v198, s20, v13
	v_med3_f32 v199, v199, s20, v13
	v_med3_f32 v200, v200, s20, v13
	v_med3_f32 v201, v201, s20, v13
	v_med3_f32 v202, v202, s20, v13
	v_med3_f32 v203, v203, s20, v13
	v_mov_b32_e32 v208, 0
	v_mov_b32_e32 v209, 0
	v_mov_b32_e32 v210, 0
	v_mov_b32_e32 v211, 0
	v_cvt_pk_fp8_f32 v208, v170, v171
	v_cvt_pk_fp8_f32 v209, v174, v175
	v_cvt_pk_fp8_f32 v210, v196, v197
	v_cvt_pk_fp8_f32 v211, v200, v201
	v_cvt_pk_fp8_f32 v208, v172, v173 op_sel:[0,0,1]
	v_cvt_pk_fp8_f32 v209, v176, v177 op_sel:[0,0,1]
	v_cvt_pk_fp8_f32 v210, v198, v199 op_sel:[0,0,1]
	v_cvt_pk_fp8_f32 v211, v202, v203 op_sel:[0,0,1]
	s_nop 0
	global_store_dwordx4 v12, v[208:211], s[14:15]
	s_waitcnt vmcnt(32)
	v_mul_f32_e32 v68, 0x43000000, v68
	v_mul_f32_e32 v69, 0x43000000, v69
	v_mul_f32_e32 v70, 0x43000000, v70
	v_mul_f32_e32 v71, 0x43000000, v71
	ds_write_b128 v5, v[68:71]
	v_mul_f32_e32 v72, 0x43000000, v72
	v_mul_f32_e32 v73, 0x43000000, v73
	v_mul_f32_e32 v74, 0x43000000, v74
	v_mul_f32_e32 v75, 0x43000000, v75
	ds_write_b128 v5, v[72:75] offset:1024
	v_mul_f32_e32 v76, 0x43000000, v76
	v_mul_f32_e32 v77, 0x43000000, v77
	v_mul_f32_e32 v78, 0x43000000, v78
	v_mul_f32_e32 v79, 0x43000000, v79
	ds_write_b128 v5, v[76:79] offset:2048
	v_mul_f32_e32 v80, 0x43000000, v80
	v_mul_f32_e32 v81, 0x43000000, v81
	v_mul_f32_e32 v82, 0x43000000, v82
	v_mul_f32_e32 v83, 0x43000000, v83
	ds_write_b128 v5, v[80:83] offset:3072
	v_mul_f32_e32 v84, 0x43000000, v84
	v_mul_f32_e32 v85, 0x43000000, v85
	v_mul_f32_e32 v86, 0x43000000, v86
	v_mul_f32_e32 v87, 0x43000000, v87
	ds_write_b128 v5, v[84:87] offset:4096
	v_mul_f32_e32 v88, 0x43000000, v88
	v_mul_f32_e32 v89, 0x43000000, v89
	v_mul_f32_e32 v90, 0x43000000, v90
	v_mul_f32_e32 v91, 0x43000000, v91
	ds_write_b128 v5, v[88:91] offset:5120
	v_mul_f32_e32 v92, 0x43000000, v92
	v_mul_f32_e32 v93, 0x43000000, v93
	v_mul_f32_e32 v94, 0x43000000, v94
	v_mul_f32_e32 v95, 0x43000000, v95
	ds_write_b128 v5, v[92:95] offset:6144
	v_mul_f32_e32 v96, 0x43000000, v96
	v_mul_f32_e32 v97, 0x43000000, v97
	v_mul_f32_e32 v98, 0x43000000, v98
	v_mul_f32_e32 v99, 0x43000000, v99
	ds_write_b128 v5, v[96:99] offset:7168
	s_waitcnt lgkmcnt(0)
	s_barrier
; #define GAS __attribute__((address_space(1)))
; #define LAS __attribute__((address_space(3)))
; #define LDS_WAIT() asm volatile("s_waitcnt lgkmcnt(0)" ::: "memory")
;     const int pr = item >> 1, kb = 2 * (pr / nblk) + (item & 1), nb = pr % nblk, k0 = 64 * kb, n0 = 32 * nb;
;     const int nr = n0 + (lane & 31); const int sc = MAP == 1 ? src_col_in(nr) : nr;
;     float v[32];
; #pragma unroll
;     for (int i = 0; i < 32; ++i) v[i] = sc >= 0 ? W[(size_t)(k0 + 2 * i + (lane >> 5)) * Nsrc + sc] : 0.f;
; #pragma unroll
;     for (int i = 0; i < 32; ++i) { const int k = k0 + 2 * i + (lane >> 5); float x = v[i] * wscale; if (KS) x *= (k < ksplit ? ksA[k] : ksB[k - ksplit]); scr[(2 * i + (lane >> 5)) * 33 + (lane & 31)] = x; }
;     LDS_WAIT(); asm volatile("" ::: "memory");
;     const int c = lane & 7;
; #pragma unroll
;     for (int j = 0; j < 4; ++j) { const int n = (lane >> 3) + 8 * j; const LAS float* s = scr + (8 * c) * 33 + n;
;         const unsigned long long o = (unsigned long long)pg8::pk4_fp8(s[0 * 33], s[1 * 33], s[2 * 33], s[3 * 33]) | ((unsigned long long)pg8::pk4_fp8(s[4 * 33], s[5 * 33], s[6 * 33], s[7 * 33]) << 32);
;         *(GAS unsigned long long*)(WT + (size_t)(n0 + n) * K + k0 + 8 * c) = o; }
;     LDS_WAIT(); asm volatile("" ::: "memory");
; }
; __global__ void __launch_bounds__(NWAVES * 64, 2) hybrid_fwd(Args args) {
;     ...
;             p0_transpose_item_f8<false>(args.in[16] + (size_t)l * FF * DM, FF, DM, DM / 32, (unsigned char*)(ws + WS_WDN + l * SZ_WDN), 128.f, args.in[16], args.in[16], 0, scr, r, lane);
	s_add_i32 s17, s16, 2784
	s_min_u32 s17, s17, 0xfff
	s_lshr_b32 s18, s17, 5
	s_add_i32 s18, s18, 0
	s_and_b32 s19, s17, 31
	s_lshl_b32 s18, s18, 21
	s_lshl_b32 s19, s19, 9
	s_add_u32 s18, s18, s19
	s_add_u32 s12, s2, s18
	s_addc_u32 s13, s3, 0
	global_load_dwordx4 v[68:71], v10, s[12:13]
	s_add_u32 s12, s12, 0x8000
	s_addc_u32 s13, s13, 0
	global_load_dwordx4 v[72:75], v10, s[12:13]
	s_add_u32 s12, s12, 0x8000
	s_addc_u32 s13, s13, 0
	global_load_dwordx4 v[76:79], v10, s[12:13]
	s_add_u32 s12, s12, 0x8000
	s_addc_u32 s13, s13, 0
	global_load_dwordx4 v[80:83], v10, s[12:13]
	s_add_u32 s12, s12, 0x8000
	s_addc_u32 s13, s13, 0
	global_load_dwordx4 v[84:87], v10, s[12:13]
	s_add_u32 s12, s12, 0x8000
	s_addc_u32 s13, s13, 0
	global_load_dwordx4 v[88:91], v10, s[12:13]
	s_add_u32 s12, s12, 0x8000
	s_addc_u32 s13, s13, 0
	global_load_dwordx4 v[92:95], v10, s[12:13]
	s_add_u32 s12, s12, 0x8000
	s_addc_u32 s13, s13, 0
	global_load_dwordx4 v[96:99], v10, s[12:13]
	s_add_i32 s17, s16, 2400
	s_min_u32 s17, s17, 0xfff
	s_lshr_b32 s18, s17, 5
	s_add_i32 s18, s18, 0
	s_and_b32 s19, s17, 31
	s_lshl_b32 s19, s19, 21
	s_lshl_b32 s18, s18, 7
	s_add_u32 s18, s18, s19
	s_add_u32 s14, s4, s18
	s_addc_u32 s15, s5, 0
	ds_read_b32 v170, v7
	ds_read_b32 v171, v7 offset:512
	ds_read_b32 v172, v7 offset:1024
	ds_read_b32 v173, v7 offset:1536
	ds_read_b32 v174, v7 offset:2048
	ds_read_b32 v175, v7 offset:2560
	ds_read_b32 v176, v7 offset:3072
	ds_read_b32 v177, v7 offset:3584
	ds_read_b32 v196, v7 offset:4096
	ds_read_b32 v197, v7 offset:4608
	ds_read_b32 v198, v7 offset:5120
	ds_read_b32 v199, v7 offset:5632
	ds_read_b32 v200, v7 offset:6144
	ds_read_b32 v201, v7 offset:6656
	ds_read_b32 v202, v7 offset:7168
	ds_read_b32 v203, v7 offset:7680
	s_waitcnt lgkmcnt(0)
	v_max_f32_e32 v170, v170, v170
	v_max_f32_e32 v171, v171, v171
	v_max_f32_e32 v172, v172, v172
	v_max_f32_e32 v173, v173, v173
	v_max_f32_e32 v174, v174, v174
	v_max_f32_e32 v175, v175, v175
	v_max_f32_e32 v176, v176, v176
	v_max_f32_e32 v177, v177, v177
	v_max_f32_e32 v196, v196, v196
	v_max_f32_e32 v197, v197, v197
	v_max_f32_e32 v198, v198, v198
	v_max_f32_e32 v199, v199, v199
	v_max_f32_e32 v200, v200, v200
	v_max_f32_e32 v201, v201, v201
	v_max_f32_e32 v202, v202, v202
	v_max_f32_e32 v203, v203, v203
	v_med3_f32 v170, v170, s20, v13
	v_med3_f32 v171, v171, s20, v13
	v_med3_f32 v172, v172, s20, v13
	v_med3_f32 v173, v173, s20, v13
	v_med3_f32 v174, v174, s20, v13
	v_med3_f32 v175, v175, s20, v13
	v_med3_f32 v176, v176, s20, v13
	v_med3_f32 v177, v177, s20, v13
	v_med3_f32 v196, v196, s20, v13
	v_med3_f32 v197, v197, s20, v13
	v_med3_f32 v198, v198, s20, v13
	v_med3_f32 v199, v199, s20, v13
	v_med3_f32 v200, v200, s20, v13
	v_med3_f32 v201, v201, s20, v13
	v_med3_f32 v202, v202, s20, v13
	v_med3_f32 v203, v203, s20, v13
	v_mov_b32_e32 v208, 0
	v_mov_b32_e32 v209, 0
	v_mov_b32_e32 v210, 0
	v_mov_b32_e32 v211, 0
	v_cvt_pk_fp8_f32 v208, v170, v171
	v_cvt_pk_fp8_f32 v209, v174, v175
	v_cvt_pk_fp8_f32 v210, v196, v197
	v_cvt_pk_fp8_f32 v211, v200, v201
	v_cvt_pk_fp8_f32 v208, v172, v173 op_sel:[0,0,1]
	v_cvt_pk_fp8_f32 v209, v176, v177 op_sel:[0,0,1]
	v_cvt_pk_fp8_f32 v210, v198, v199 op_sel:[0,0,1]
	v_cvt_pk_fp8_f32 v211, v202, v203 op_sel:[0,0,1]
	s_nop 0
	global_store_dwordx4 v11, v[208:211], s[14:15]
	ds_read_b32 v170, v9
	ds_read_b32 v171, v9 offset:512
	ds_read_b32 v172, v9 offset:1024
	ds_read_b32 v173, v9 offset:1536
	ds_read_b32 v174, v9 offset:2048
	ds_read_b32 v175, v9 offset:2560
	ds_read_b32 v176, v9 offset:3072
	ds_read_b32 v177, v9 offset:3584
	ds_read_b32 v196, v9 offset:4096
	ds_read_b32 v197, v9 offset:4608
	ds_read_b32 v198, v9 offset:5120
	ds_read_b32 v199, v9 offset:5632
	ds_read_b32 v200, v9 offset:6144
	ds_read_b32 v201, v9 offset:6656
	ds_read_b32 v202, v9 offset:7168
	ds_read_b32 v203, v9 offset:7680
	s_waitcnt lgkmcnt(0)
	v_max_f32_e32 v170, v170, v170
	v_max_f32_e32 v171, v171, v171
	v_max_f32_e32 v172, v172, v172
	v_max_f32_e32 v173, v173, v173
	v_max_f32_e32 v174, v174, v174
	v_max_f32_e32 v175, v175, v175
	v_max_f32_e32 v176, v176, v176
	v_max_f32_e32 v177, v177, v177
	v_max_f32_e32 v196, v196, v196
	v_max_f32_e32 v197, v197, v197
	v_max_f32_e32 v198, v198, v198
	v_max_f32_e32 v199, v199, v199
	v_max_f32_e32 v200, v200, v200
	v_max_f32_e32 v201, v201, v201
	v_max_f32_e32 v202, v202, v202
	v_max_f32_e32 v203, v203, v203
	v_med3_f32 v170, v170, s20, v13
	v_med3_f32 v171, v171, s20, v13
	v_med3_f32 v172, v172, s20, v13
	v_med3_f32 v173, v173, s20, v13
	v_med3_f32 v174, v174, s20, v13
	v_med3_f32 v175, v175, s20, v13
	v_med3_f32 v176, v176, s20, v13
	v_med3_f32 v177, v177, s20, v13
	v_med3_f32 v196, v196, s20, v13
	v_med3_f32 v197, v197, s20, v13
	v_med3_f32 v198, v198, s20, v13
	v_med3_f32 v199, v199, s20, v13
	v_med3_f32 v200, v200, s20, v13
	v_med3_f32 v201, v201, s20, v13
	v_med3_f32 v202, v202, s20, v13
	v_med3_f32 v203, v203, s20, v13
	v_mov_b32_e32 v208, 0
	v_mov_b32_e32 v209, 0
	v_mov_b32_e32 v210, 0
	v_mov_b32_e32 v211, 0
	v_cvt_pk_fp8_f32 v208, v170, v171
	v_cvt_pk_fp8_f32 v209, v174, v175
	v_cvt_pk_fp8_f32 v210, v196, v197
	v_cvt_pk_fp8_f32 v211, v200, v201
	v_cvt_pk_fp8_f32 v208, v172, v173 op_sel:[0,0,1]
	v_cvt_pk_fp8_f32 v209, v176, v177 op_sel:[0,0,1]
	v_cvt_pk_fp8_f32 v210, v198, v199 op_sel:[0,0,1]
	v_cvt_pk_fp8_f32 v211, v202, v203 op_sel:[0,0,1]
	s_nop 0
	global_store_dwordx4 v12, v[208:211], s[14:15]
	s_waitcnt vmcnt(32)
	v_mul_f32_e32 v100, 0x43000000, v100
	v_mul_f32_e32 v101, 0x43000000, v101
	v_mul_f32_e32 v102, 0x43000000, v102
	v_mul_f32_e32 v103, 0x43000000, v103
	ds_write_b128 v4, v[100:103]
	v_mul_f32_e32 v104, 0x43000000, v104
	v_mul_f32_e32 v105, 0x43000000, v105
	v_mul_f32_e32 v106, 0x43000000, v106
	v_mul_f32_e32 v107, 0x43000000, v107
	ds_write_b128 v4, v[104:107] offset:1024
	v_mul_f32_e32 v108, 0x43000000, v108
	v_mul_f32_e32 v109, 0x43000000, v109
	v_mul_f32_e32 v110, 0x43000000, v110
	v_mul_f32_e32 v111, 0x43000000, v111
	ds_write_b128 v4, v[108:111] offset:2048
	v_mul_f32_e32 v112, 0x43000000, v112
	v_mul_f32_e32 v113, 0x43000000, v113
	v_mul_f32_e32 v114, 0x43000000, v114
	v_mul_f32_e32 v115, 0x43000000, v115
	ds_write_b128 v4, v[112:115] offset:3072
	v_mul_f32_e32 v116, 0x43000000, v116
	v_mul_f32_e32 v117, 0x43000000, v117
	v_mul_f32_e32 v118, 0x43000000, v118
	v_mul_f32_e32 v119, 0x43000000, v119
	ds_write_b128 v4, v[116:119] offset:4096
	v_mul_f32_e32 v120, 0x43000000, v120
	v_mul_f32_e32 v121, 0x43000000, v121
	v_mul_f32_e32 v122, 0x43000000, v122
	v_mul_f32_e32 v123, 0x43000000, v123
	ds_write_b128 v4, v[120:123] offset:5120
	v_mul_f32_e32 v124, 0x43000000, v124
	v_mul_f32_e32 v125, 0x43000000, v125
	v_mul_f32_e32 v126, 0x43000000, v126
	v_mul_f32_e32 v127, 0x43000000, v127
	ds_write_b128 v4, v[124:127] offset:6144
	v_mul_f32_e32 v128, 0x43000000, v128
	v_mul_f32_e32 v129, 0x43000000, v129
	v_mul_f32_e32 v130, 0x43000000, v130
	v_mul_f32_e32 v131, 0x43000000, v131
	ds_write_b128 v4, v[128:131] offset:7168
	s_waitcnt lgkmcnt(0)
	s_barrier
; #define GAS __attribute__((address_space(1)))
; #define LAS __attribute__((address_space(3)))
; #define LDS_WAIT() asm volatile("s_waitcnt lgkmcnt(0)" ::: "memory")
;     const int pr = item >> 1, kb = 2 * (pr / nblk) + (item & 1), nb = pr % nblk, k0 = 64 * kb, n0 = 32 * nb;
;     const int nr = n0 + (lane & 31); const int sc = MAP == 1 ? src_col_in(nr) : nr;
;     float v[32];
; #pragma unroll
;     for (int i = 0; i < 32; ++i) v[i] = sc >= 0 ? W[(size_t)(k0 + 2 * i + (lane >> 5)) * Nsrc + sc] : 0.f;
; #pragma unroll
;     for (int i = 0; i < 32; ++i) { const int k = k0 + 2 * i + (lane >> 5); float x = v[i] * wscale; if (KS) x *= (k < ksplit ? ksA[k] : ksB[k - ksplit]); scr[(2 * i + (lane >> 5)) * 33 + (lane & 31)] = x; }
;     LDS_WAIT(); asm volatile("" ::: "memory");
;     const int c = lane & 7;
; #pragma unroll
;     for (int j = 0; j < 4; ++j) { const int n = (lane >> 3) + 8 * j; const LAS float* s = scr + (8 * c) * 33 + n;
;         const unsigned long long o = (unsigned long long)pg8::pk4_fp8(s[0 * 33], s[1 * 33], s[2 * 33], s[3 * 33]) | ((unsigned long long)pg8::pk4_fp8(s[4 * 33], s[5 * 33], s[6 * 33], s[7 * 33]) << 32);
;         *(GAS unsigned long long*)(WT + (size_t)(n0 + n) * K + k0 + 8 * c) = o; }
;     LDS_WAIT(); asm volatile("" ::: "memory");
; }
; __global__ void __launch_bounds__(NWAVES * 64, 2) hybrid_fwd(Args args) {
;     ...
;             p0_transpose_item_f8<false>(args.in[16] + (size_t)l * FF * DM, FF, DM, DM / 32, (unsigned char*)(ws + WS_WDN + l * SZ_WDN), 128.f, args.in[16], args.in[16], 0, scr, r, lane);
	s_add_i32 s17, s16, 2880
	s_min_u32 s17, s17, 0xfff
	s_lshr_b32 s18, s17, 5
	s_add_i32 s18, s18, 0
	s_and_b32 s19, s17, 31
	s_lshl_b32 s18, s18, 21
	s_lshl_b32 s19, s19, 9
	s_add_u32 s18, s18, s19
	s_add_u32 s12, s2, s18
	s_addc_u32 s13, s3, 0
	global_load_dwordx4 v[100:103], v10, s[12:13]
	s_add_u32 s12, s12, 0x8000
	s_addc_u32 s13, s13, 0
	global_load_dwordx4 v[104:107], v10, s[12:13]
	s_add_u32 s12, s12, 0x8000
	s_addc_u32 s13, s13, 0
	global_load_dwordx4 v[108:111], v10, s[12:13]
	s_add_u32 s12, s12, 0x8000
	s_addc_u32 s13, s13, 0
	global_load_dwordx4 v[112:115], v10, s[12:13]
	s_add_u32 s12, s12, 0x8000
	s_addc_u32 s13, s13, 0
	global_load_dwordx4 v[116:119], v10, s[12:13]
	s_add_u32 s12, s12, 0x8000
	s_addc_u32 s13, s13, 0
	global_load_dwordx4 v[120:123], v10, s[12:13]
	s_add_u32 s12, s12, 0x8000
	s_addc_u32 s13, s13, 0
	global_load_dwordx4 v[124:127], v10, s[12:13]
	s_add_u32 s12, s12, 0x8000
	s_addc_u32 s13, s13, 0
	global_load_dwordx4 v[128:131], v10, s[12:13]
	s_add_i32 s17, s16, 2496
	s_min_u32 s17, s17, 0xfff
	s_lshr_b32 s18, s17, 5
	s_add_i32 s18, s18, 0
	s_and_b32 s19, s17, 31
	s_lshl_b32 s19, s19, 21
	s_lshl_b32 s18, s18, 7
	s_add_u32 s18, s18, s19
	s_add_u32 s14, s4, s18
	s_addc_u32 s15, s5, 0
	ds_read_b32 v170, v6
	ds_read_b32 v171, v6 offset:512
	ds_read_b32 v172, v6 offset:1024
	ds_read_b32 v173, v6 offset:1536
	ds_read_b32 v174, v6 offset:2048
	ds_read_b32 v175, v6 offset:2560
	ds_read_b32 v176, v6 offset:3072
	ds_read_b32 v177, v6 offset:3584
	ds_read_b32 v196, v6 offset:4096
	ds_read_b32 v197, v6 offset:4608
	ds_read_b32 v198, v6 offset:5120
	ds_read_b32 v199, v6 offset:5632
	ds_read_b32 v200, v6 offset:6144
	ds_read_b32 v201, v6 offset:6656
	ds_read_b32 v202, v6 offset:7168
	ds_read_b32 v203, v6 offset:7680
	s_waitcnt lgkmcnt(0)
	v_max_f32_e32 v170, v170, v170
	v_max_f32_e32 v171, v171, v171
	v_max_f32_e32 v172, v172, v172
	v_max_f32_e32 v173, v173, v173
	v_max_f32_e32 v174, v174, v174
	v_max_f32_e32 v175, v175, v175
	v_max_f32_e32 v176, v176, v176
	v_max_f32_e32 v177, v177, v177
	v_max_f32_e32 v196, v196, v196
	v_max_f32_e32 v197, v197, v197
	v_max_f32_e32 v198, v198, v198
	v_max_f32_e32 v199, v199, v199
	v_max_f32_e32 v200, v200, v200
	v_max_f32_e32 v201, v201, v201
	v_max_f32_e32 v202, v202, v202
	v_max_f32_e32 v203, v203, v203
	v_med3_f32 v170, v170, s20, v13
	v_med3_f32 v171, v171, s20, v13
	v_med3_f32 v172, v172, s20, v13
	v_med3_f32 v173, v173, s20, v13
	v_med3_f32 v174, v174, s20, v13
	v_med3_f32 v175, v175, s20, v13
	v_med3_f32 v176, v176, s20, v13
	v_med3_f32 v177, v177, s20, v13
	v_med3_f32 v196, v196, s20, v13
	v_med3_f32 v197, v197, s20, v13
	v_med3_f32 v198, v198, s20, v13
	v_med3_f32 v199, v199, s20, v13
	v_med3_f32 v200, v200, s20, v13
	v_med3_f32 v201, v201, s20, v13
	v_med3_f32 v202, v202, s20, v13
	v_med3_f32 v203, v203, s20, v13
	v_mov_b32_e32 v208, 0
	v_mov_b32_e32 v209, 0
	v_mov_b32_e32 v210, 0
	v_mov_b32_e32 v211, 0
	v_cvt_pk_fp8_f32 v208, v170, v171
	v_cvt_pk_fp8_f32 v209, v174, v175
	v_cvt_pk_fp8_f32 v210, v196, v197
	v_cvt_pk_fp8_f32 v211, v200, v201
	v_cvt_pk_fp8_f32 v208, v172, v173 op_sel:[0,0,1]
	v_cvt_pk_fp8_f32 v209, v176, v177 op_sel:[0,0,1]
	v_cvt_pk_fp8_f32 v210, v198, v199 op_sel:[0,0,1]
	v_cvt_pk_fp8_f32 v211, v202, v203 op_sel:[0,0,1]
	s_nop 0
	global_store_dwordx4 v11, v[208:211], s[14:15]
	ds_read_b32 v170, v8
	ds_read_b32 v171, v8 offset:512
	ds_read_b32 v172, v8 offset:1024
	ds_read_b32 v173, v8 offset:1536
	ds_read_b32 v174, v8 offset:2048
	ds_read_b32 v175, v8 offset:2560
	ds_read_b32 v176, v8 offset:3072
	ds_read_b32 v177, v8 offset:3584
	ds_read_b32 v196, v8 offset:4096
	ds_read_b32 v197, v8 offset:4608
	ds_read_b32 v198, v8 offset:5120
	ds_read_b32 v199, v8 offset:5632
	ds_read_b32 v200, v8 offset:6144
	ds_read_b32 v201, v8 offset:6656
	ds_read_b32 v202, v8 offset:7168
	ds_read_b32 v203, v8 offset:7680
	s_waitcnt lgkmcnt(0)
	v_max_f32_e32 v170, v170, v170
	v_max_f32_e32 v171, v171, v171
	v_max_f32_e32 v172, v172, v172
	v_max_f32_e32 v173, v173, v173
	v_max_f32_e32 v174, v174, v174
	v_max_f32_e32 v175, v175, v175
	v_max_f32_e32 v176, v176, v176
	v_max_f32_e32 v177, v177, v177
	v_max_f32_e32 v196, v196, v196
	v_max_f32_e32 v197, v197, v197
	v_max_f32_e32 v198, v198, v198
	v_max_f32_e32 v199, v199, v199
	v_max_f32_e32 v200, v200, v200
	v_max_f32_e32 v201, v201, v201
	v_max_f32_e32 v202, v202, v202
	v_max_f32_e32 v203, v203, v203
	v_med3_f32 v170, v170, s20, v13
	v_med3_f32 v171, v171, s20, v13
	v_med3_f32 v172, v172, s20, v13
	v_med3_f32 v173, v173, s20, v13
	v_med3_f32 v174, v174, s20, v13
	v_med3_f32 v175, v175, s20, v13
	v_med3_f32 v176, v176, s20, v13
	v_med3_f32 v177, v177, s20, v13
	v_med3_f32 v196, v196, s20, v13
	v_med3_f32 v197, v197, s20, v13
	v_med3_f32 v198, v198, s20, v13
	v_med3_f32 v199, v199, s20, v13
	v_med3_f32 v200, v200, s20, v13
	v_med3_f32 v201, v201, s20, v13
	v_med3_f32 v202, v202, s20, v13
	v_med3_f32 v203, v203, s20, v13
	v_mov_b32_e32 v208, 0
	v_mov_b32_e32 v209, 0
	v_mov_b32_e32 v210, 0
	v_mov_b32_e32 v211, 0
	v_cvt_pk_fp8_f32 v208, v170, v171
	v_cvt_pk_fp8_f32 v209, v174, v175
	v_cvt_pk_fp8_f32 v210, v196, v197
	v_cvt_pk_fp8_f32 v211, v200, v201
	v_cvt_pk_fp8_f32 v208, v172, v173 op_sel:[0,0,1]
	v_cvt_pk_fp8_f32 v209, v176, v177 op_sel:[0,0,1]
	v_cvt_pk_fp8_f32 v210, v198, v199 op_sel:[0,0,1]
	v_cvt_pk_fp8_f32 v211, v202, v203 op_sel:[0,0,1]
	s_nop 0
	global_store_dwordx4 v12, v[208:211], s[14:15]
	s_waitcnt vmcnt(32)
	v_mul_f32_e32 v132, 0x43000000, v132
	v_mul_f32_e32 v133, 0x43000000, v133
	v_mul_f32_e32 v134, 0x43000000, v134
	v_mul_f32_e32 v135, 0x43000000, v135
	ds_write_b128 v5, v[132:135]
	v_mul_f32_e32 v136, 0x43000000, v136
	v_mul_f32_e32 v137, 0x43000000, v137
	v_mul_f32_e32 v138, 0x43000000, v138
	v_mul_f32_e32 v139, 0x43000000, v139
	ds_write_b128 v5, v[136:139] offset:1024
	v_mul_f32_e32 v140, 0x43000000, v140
	v_mul_f32_e32 v141, 0x43000000, v141
	v_mul_f32_e32 v142, 0x43000000, v142
	v_mul_f32_e32 v143, 0x43000000, v143
	ds_write_b128 v5, v[140:143] offset:2048
	v_mul_f32_e32 v144, 0x43000000, v144
	v_mul_f32_e32 v145, 0x43000000, v145
	v_mul_f32_e32 v146, 0x43000000, v146
	v_mul_f32_e32 v147, 0x43000000, v147
	ds_write_b128 v5, v[144:147] offset:3072
	v_mul_f32_e32 v148, 0x43000000, v148
	v_mul_f32_e32 v149, 0x43000000, v149
	v_mul_f32_e32 v150, 0x43000000, v150
	v_mul_f32_e32 v151, 0x43000000, v151
	ds_write_b128 v5, v[148:151] offset:4096
	v_mul_f32_e32 v152, 0x43000000, v152
	v_mul_f32_e32 v153, 0x43000000, v153
	v_mul_f32_e32 v154, 0x43000000, v154
	v_mul_f32_e32 v155, 0x43000000, v155
	ds_write_b128 v5, v[152:155] offset:5120
	v_mul_f32_e32 v156, 0x43000000, v156
	v_mul_f32_e32 v157, 0x43000000, v157
	v_mul_f32_e32 v158, 0x43000000, v158
	v_mul_f32_e32 v159, 0x43000000, v159
	ds_write_b128 v5, v[156:159] offset:6144
	v_mul_f32_e32 v160, 0x43000000, v160
	v_mul_f32_e32 v161, 0x43000000, v161
	v_mul_f32_e32 v162, 0x43000000, v162
	v_mul_f32_e32 v163, 0x43000000, v163
	ds_write_b128 v5, v[160:163] offset:7168
	s_waitcnt lgkmcnt(0)
	s_barrier
; #define GAS __attribute__((address_space(1)))
; #define LAS __attribute__((address_space(3)))
; #define LDS_WAIT() asm volatile("s_waitcnt lgkmcnt(0)" ::: "memory")
;     const int pr = item >> 1, kb = 2 * (pr / nblk) + (item & 1), nb = pr % nblk, k0 = 64 * kb, n0 = 32 * nb;
;     const int nr = n0 + (lane & 31); const int sc = MAP == 1 ? src_col_in(nr) : nr;
;     float v[32];
; #pragma unroll
;     for (int i = 0; i < 32; ++i) v[i] = sc >= 0 ? W[(size_t)(k0 + 2 * i + (lane >> 5)) * Nsrc + sc] : 0.f;
; #pragma unroll
;     for (int i = 0; i < 32; ++i) { const int k = k0 + 2 * i + (lane >> 5); float x = v[i] * wscale; if (KS) x *= (k < ksplit ? ksA[k] : ksB[k - ksplit]); scr[(2 * i + (lane >> 5)) * 33 + (lane & 31)] = x; }
;     LDS_WAIT(); asm volatile("" ::: "memory");
;     const int c = lane & 7;
; #pragma unroll
;     for (int j = 0; j < 4; ++j) { const int n = (lane >> 3) + 8 * j; const LAS float* s = scr + (8 * c) * 33 + n;
;         const unsigned long long o = (unsigned long long)pg8::pk4_fp8(s[0 * 33], s[1 * 33], s[2 * 33], s[3 * 33]) | ((unsigned long long)pg8::pk4_fp8(s[4 * 33], s[5 * 33], s[6 * 33], s[7 * 33]) << 32);
;         *(GAS unsigned long long*)(WT + (size_t)(n0 + n) * K + k0 + 8 * c) = o; }
;     LDS_WAIT(); asm volatile("" ::: "memory");
; }
; __global__ void __launch_bounds__(NWAVES * 64, 2) hybrid_fwd(Args args) {
;     ...
;             p0_transpose_item_f8<false>(args.in[16] + (size_t)l * FF * DM, FF, DM, DM / 32, (unsigned char*)(ws + WS_WDN + l * SZ_WDN), 128.f, args.in[16], args.in[16], 0, scr, r, lane);
	s_add_i32 s17, s16, 2976
	s_min_u32 s17, s17, 0xfff
	s_lshr_b32 s18, s17, 5
	s_add_i32 s18, s18, 0
	s_and_b32 s19, s17, 31
	s_lshl_b32 s18, s18, 21
	s_lshl_b32 s19, s19, 9
	s_add_u32 s18, s18, s19
	s_add_u32 s12, s2, s18
	s_addc_u32 s13, s3, 0
	global_load_dwordx4 v[132:135], v10, s[12:13]
	s_add_u32 s12, s12, 0x8000
	s_addc_u32 s13, s13, 0
	global_load_dwordx4 v[136:139], v10, s[12:13]
	s_add_u32 s12, s12, 0x8000
	s_addc_u32 s13, s13, 0
	global_load_dwordx4 v[140:143], v10, s[12:13]
	s_add_u32 s12, s12, 0x8000
	s_addc_u32 s13, s13, 0
	global_load_dwordx4 v[144:147], v10, s[12:13]
	s_add_u32 s12, s12, 0x8000
	s_addc_u32 s13, s13, 0
	global_load_dwordx4 v[148:151], v10, s[12:13]
	s_add_u32 s12, s12, 0x8000
	s_addc_u32 s13, s13, 0
	global_load_dwordx4 v[152:155], v10, s[12:13]
	s_add_u32 s12, s12, 0x8000
	s_addc_u32 s13, s13, 0
	global_load_dwordx4 v[156:159], v10, s[12:13]
	s_add_u32 s12, s12, 0x8000
	s_addc_u32 s13, s13, 0
	global_load_dwordx4 v[160:163], v10, s[12:13]
	s_add_i32 s17, s16, 2592
	s_min_u32 s17, s17, 0xfff
	s_lshr_b32 s18, s17, 5
	s_add_i32 s18, s18, 0
	s_and_b32 s19, s17, 31
	s_lshl_b32 s19, s19, 21
	s_lshl_b32 s18, s18, 7
	s_add_u32 s18, s18, s19
	s_add_u32 s14, s4, s18
	s_addc_u32 s15, s5, 0
	ds_read_b32 v170, v7
	ds_read_b32 v171, v7 offset:512
	ds_read_b32 v172, v7 offset:1024
	ds_read_b32 v173, v7 offset:1536
	ds_read_b32 v174, v7 offset:2048
	ds_read_b32 v175, v7 offset:2560
	ds_read_b32 v176, v7 offset:3072
	ds_read_b32 v177, v7 offset:3584
	ds_read_b32 v196, v7 offset:4096
	ds_read_b32 v197, v7 offset:4608
	ds_read_b32 v198, v7 offset:5120
	ds_read_b32 v199, v7 offset:5632
	ds_read_b32 v200, v7 offset:6144
	ds_read_b32 v201, v7 offset:6656
	ds_read_b32 v202, v7 offset:7168
	ds_read_b32 v203, v7 offset:7680
	s_waitcnt lgkmcnt(0)
	v_max_f32_e32 v170, v170, v170
	v_max_f32_e32 v171, v171, v171
	v_max_f32_e32 v172, v172, v172
	v_max_f32_e32 v173, v173, v173
	v_max_f32_e32 v174, v174, v174
	v_max_f32_e32 v175, v175, v175
	v_max_f32_e32 v176, v176, v176
	v_max_f32_e32 v177, v177, v177
	v_max_f32_e32 v196, v196, v196
	v_max_f32_e32 v197, v197, v197
	v_max_f32_e32 v198, v198, v198
	v_max_f32_e32 v199, v199, v199
	v_max_f32_e32 v200, v200, v200
	v_max_f32_e32 v201, v201, v201
	v_max_f32_e32 v202, v202, v202
	v_max_f32_e32 v203, v203, v203
	v_med3_f32 v170, v170, s20, v13
	v_med3_f32 v171, v171, s20, v13
	v_med3_f32 v172, v172, s20, v13
	v_med3_f32 v173, v173, s20, v13
	v_med3_f32 v174, v174, s20, v13
	v_med3_f32 v175, v175, s20, v13
	v_med3_f32 v176, v176, s20, v13
	v_med3_f32 v177, v177, s20, v13
	v_med3_f32 v196, v196, s20, v13
	v_med3_f32 v197, v197, s20, v13
	v_med3_f32 v198, v198, s20, v13
	v_med3_f32 v199, v199, s20, v13
	v_med3_f32 v200, v200, s20, v13
	v_med3_f32 v201, v201, s20, v13
	v_med3_f32 v202, v202, s20, v13
	v_med3_f32 v203, v203, s20, v13
	v_mov_b32_e32 v208, 0
	v_mov_b32_e32 v209, 0
	v_mov_b32_e32 v210, 0
	v_mov_b32_e32 v211, 0
	v_cvt_pk_fp8_f32 v208, v170, v171
	v_cvt_pk_fp8_f32 v209, v174, v175
	v_cvt_pk_fp8_f32 v210, v196, v197
	v_cvt_pk_fp8_f32 v211, v200, v201
	v_cvt_pk_fp8_f32 v208, v172, v173 op_sel:[0,0,1]
	v_cvt_pk_fp8_f32 v209, v176, v177 op_sel:[0,0,1]
	v_cvt_pk_fp8_f32 v210, v198, v199 op_sel:[0,0,1]
	v_cvt_pk_fp8_f32 v211, v202, v203 op_sel:[0,0,1]
	s_nop 0
	global_store_dwordx4 v11, v[208:211], s[14:15]
	ds_read_b32 v170, v9
	ds_read_b32 v171, v9 offset:512
	ds_read_b32 v172, v9 offset:1024
	ds_read_b32 v173, v9 offset:1536
	ds_read_b32 v174, v9 offset:2048
	ds_read_b32 v175, v9 offset:2560
	ds_read_b32 v176, v9 offset:3072
	ds_read_b32 v177, v9 offset:3584
	ds_read_b32 v196, v9 offset:4096
	ds_read_b32 v197, v9 offset:4608
	ds_read_b32 v198, v9 offset:5120
	ds_read_b32 v199, v9 offset:5632
	ds_read_b32 v200, v9 offset:6144
	ds_read_b32 v201, v9 offset:6656
	ds_read_b32 v202, v9 offset:7168
	ds_read_b32 v203, v9 offset:7680
	s_waitcnt lgkmcnt(0)
	v_max_f32_e32 v170, v170, v170
	v_max_f32_e32 v171, v171, v171
	v_max_f32_e32 v172, v172, v172
	v_max_f32_e32 v173, v173, v173
	v_max_f32_e32 v174, v174, v174
	v_max_f32_e32 v175, v175, v175
	v_max_f32_e32 v176, v176, v176
	v_max_f32_e32 v177, v177, v177
	v_max_f32_e32 v196, v196, v196
	v_max_f32_e32 v197, v197, v197
	v_max_f32_e32 v198, v198, v198
	v_max_f32_e32 v199, v199, v199
	v_max_f32_e32 v200, v200, v200
	v_max_f32_e32 v201, v201, v201
	v_max_f32_e32 v202, v202, v202
	v_max_f32_e32 v203, v203, v203
	v_med3_f32 v170, v170, s20, v13
	v_med3_f32 v171, v171, s20, v13
	v_med3_f32 v172, v172, s20, v13
	v_med3_f32 v173, v173, s20, v13
	v_med3_f32 v174, v174, s20, v13
	v_med3_f32 v175, v175, s20, v13
	v_med3_f32 v176, v176, s20, v13
	v_med3_f32 v177, v177, s20, v13
	v_med3_f32 v196, v196, s20, v13
	v_med3_f32 v197, v197, s20, v13
	v_med3_f32 v198, v198, s20, v13
	v_med3_f32 v199, v199, s20, v13
	v_med3_f32 v200, v200, s20, v13
	v_med3_f32 v201, v201, s20, v13
	v_med3_f32 v202, v202, s20, v13
	v_med3_f32 v203, v203, s20, v13
	v_mov_b32_e32 v208, 0
	v_mov_b32_e32 v209, 0
	v_mov_b32_e32 v210, 0
	v_mov_b32_e32 v211, 0
	v_cvt_pk_fp8_f32 v208, v170, v171
	v_cvt_pk_fp8_f32 v209, v174, v175
	v_cvt_pk_fp8_f32 v210, v196, v197
	v_cvt_pk_fp8_f32 v211, v200, v201
	v_cvt_pk_fp8_f32 v208, v172, v173 op_sel:[0,0,1]
	v_cvt_pk_fp8_f32 v209, v176, v177 op_sel:[0,0,1]
	v_cvt_pk_fp8_f32 v210, v198, v199 op_sel:[0,0,1]
	v_cvt_pk_fp8_f32 v211, v202, v203 op_sel:[0,0,1]
	s_nop 0
	global_store_dwordx4 v12, v[208:211], s[14:15]
	s_waitcnt vmcnt(32)
	v_mul_f32_e32 v36, 0x43000000, v36
	v_mul_f32_e32 v37, 0x43000000, v37
	v_mul_f32_e32 v38, 0x43000000, v38
	v_mul_f32_e32 v39, 0x43000000, v39
	ds_write_b128 v4, v[36:39]
	v_mul_f32_e32 v40, 0x43000000, v40
	v_mul_f32_e32 v41, 0x43000000, v41
	v_mul_f32_e32 v42, 0x43000000, v42
	v_mul_f32_e32 v43, 0x43000000, v43
	ds_write_b128 v4, v[40:43] offset:1024
	v_mul_f32_e32 v44, 0x43000000, v44
	v_mul_f32_e32 v45, 0x43000000, v45
	v_mul_f32_e32 v46, 0x43000000, v46
	v_mul_f32_e32 v47, 0x43000000, v47
	ds_write_b128 v4, v[44:47] offset:2048
	v_mul_f32_e32 v48, 0x43000000, v48
	v_mul_f32_e32 v49, 0x43000000, v49
	v_mul_f32_e32 v50, 0x43000000, v50
	v_mul_f32_e32 v51, 0x43000000, v51
	ds_write_b128 v4, v[48:51] offset:3072
	v_mul_f32_e32 v52, 0x43000000, v52
	v_mul_f32_e32 v53, 0x43000000, v53
	v_mul_f32_e32 v54, 0x43000000, v54
	v_mul_f32_e32 v55, 0x43000000, v55
	ds_write_b128 v4, v[52:55] offset:4096
	v_mul_f32_e32 v56, 0x43000000, v56
	v_mul_f32_e32 v57, 0x43000000, v57
	v_mul_f32_e32 v58, 0x43000000, v58
	v_mul_f32_e32 v59, 0x43000000, v59
	ds_write_b128 v4, v[56:59] offset:5120
	v_mul_f32_e32 v60, 0x43000000, v60
	v_mul_f32_e32 v61, 0x43000000, v61
	v_mul_f32_e32 v62, 0x43000000, v62
	v_mul_f32_e32 v63, 0x43000000, v63
	ds_write_b128 v4, v[60:63] offset:6144
	v_mul_f32_e32 v64, 0x43000000, v64
	v_mul_f32_e32 v65, 0x43000000, v65
	v_mul_f32_e32 v66, 0x43000000, v66
	v_mul_f32_e32 v67, 0x43000000, v67
	ds_write_b128 v4, v[64:67] offset:7168
	s_waitcnt lgkmcnt(0)
	s_barrier
; #define GAS __attribute__((address_space(1)))
; #define LAS __attribute__((address_space(3)))
; #define LDS_WAIT() asm volatile("s_waitcnt lgkmcnt(0)" ::: "memory")
;     const int pr = item >> 1, kb = 2 * (pr / nblk) + (item & 1), nb = pr % nblk, k0 = 64 * kb, n0 = 32 * nb;
;     const int nr = n0 + (lane & 31); const int sc = MAP == 1 ? src_col_in(nr) : nr;
;     float v[32];
; #pragma unroll
;     for (int i = 0; i < 32; ++i) v[i] = sc >= 0 ? W[(size_t)(k0 + 2 * i + (lane >> 5)) * Nsrc + sc] : 0.f;
; #pragma unroll
;     for (int i = 0; i < 32; ++i) { const int k = k0 + 2 * i + (lane >> 5); float x = v[i] * wscale; if (KS) x *= (k < ksplit ? ksA[k] : ksB[k - ksplit]); scr[(2 * i + (lane >> 5)) * 33 + (lane & 31)] = x; }
;     LDS_WAIT(); asm volatile("" ::: "memory");
;     const int c = lane & 7;
; #pragma unroll
;     for (int j = 0; j < 4; ++j) { const int n = (lane >> 3) + 8 * j; const LAS float* s = scr + (8 * c) * 33 + n;
;         const unsigned long long o = (unsigned long long)pg8::pk4_fp8(s[0 * 33], s[1 * 33], s[2 * 33], s[3 * 33]) | ((unsigned long long)pg8::pk4_fp8(s[4 * 33], s[5 * 33], s[6 * 33], s[7 * 33]) << 32);
;         *(GAS unsigned long long*)(WT + (size_t)(n0 + n) * K + k0 + 8 * c) = o; }
;     LDS_WAIT(); asm volatile("" ::: "memory");
; }
; __global__ void __launch_bounds__(NWAVES * 64, 2) hybrid_fwd(Args args) {
;     ...
;             p0_transpose_item_f8<false>(args.in[16] + (size_t)l * FF * DM, FF, DM, DM / 32, (unsigned char*)(ws + WS_WDN + l * SZ_WDN), 128.f, args.in[16], args.in[16], 0, scr, r, lane);
	s_add_i32 s17, s16, 3072
	s_min_u32 s17, s17, 0xfff
	s_lshr_b32 s18, s17, 5
	s_add_i32 s18, s18, 0
	s_and_b32 s19, s17, 31
	s_lshl_b32 s18, s18, 21
	s_lshl_b32 s19, s19, 9
	s_add_u32 s18, s18, s19
	s_add_u32 s12, s2, s18
	s_addc_u32 s13, s3, 0
	global_load_dwordx4 v[36:39], v10, s[12:13]
	s_add_u32 s12, s12, 0x8000
	s_addc_u32 s13, s13, 0
	global_load_dwordx4 v[40:43], v10, s[12:13]
	s_add_u32 s12, s12, 0x8000
	s_addc_u32 s13, s13, 0
	global_load_dwordx4 v[44:47], v10, s[12:13]
	s_add_u32 s12, s12, 0x8000
	s_addc_u32 s13, s13, 0
	global_load_dwordx4 v[48:51], v10, s[12:13]
	s_add_u32 s12, s12, 0x8000
	s_addc_u32 s13, s13, 0
	global_load_dwordx4 v[52:55], v10, s[12:13]
	s_add_u32 s12, s12, 0x8000
	s_addc_u32 s13, s13, 0
	global_load_dwordx4 v[56:59], v10, s[12:13]
	s_add_u32 s12, s12, 0x8000
	s_addc_u32 s13, s13, 0
	global_load_dwordx4 v[60:63], v10, s[12:13]
	s_add_u32 s12, s12, 0x8000
	s_addc_u32 s13, s13, 0
	global_load_dwordx4 v[64:67], v10, s[12:13]
	s_add_i32 s17, s16, 2688
	s_min_u32 s17, s17, 0xfff
	s_lshr_b32 s18, s17, 5
	s_add_i32 s18, s18, 0
	s_and_b32 s19, s17, 31
	s_lshl_b32 s19, s19, 21
	s_lshl_b32 s18, s18, 7
	s_add_u32 s18, s18, s19
	s_add_u32 s14, s4, s18
	s_addc_u32 s15, s5, 0
	ds_read_b32 v170, v6
	ds_read_b32 v171, v6 offset:512
	ds_read_b32 v172, v6 offset:1024
	ds_read_b32 v173, v6 offset:1536
	ds_read_b32 v174, v6 offset:2048
	ds_read_b32 v175, v6 offset:2560
	ds_read_b32 v176, v6 offset:3072
	ds_read_b32 v177, v6 offset:3584
	ds_read_b32 v196, v6 offset:4096
	ds_read_b32 v197, v6 offset:4608
	ds_read_b32 v198, v6 offset:5120
	ds_read_b32 v199, v6 offset:5632
	ds_read_b32 v200, v6 offset:6144
	ds_read_b32 v201, v6 offset:6656
	ds_read_b32 v202, v6 offset:7168
	ds_read_b32 v203, v6 offset:7680
	s_waitcnt lgkmcnt(0)
	v_max_f32_e32 v170, v170, v170
	v_max_f32_e32 v171, v171, v171
	v_max_f32_e32 v172, v172, v172
	v_max_f32_e32 v173, v173, v173
	v_max_f32_e32 v174, v174, v174
	v_max_f32_e32 v175, v175, v175
	v_max_f32_e32 v176, v176, v176
	v_max_f32_e32 v177, v177, v177
	v_max_f32_e32 v196, v196, v196
	v_max_f32_e32 v197, v197, v197
	v_max_f32_e32 v198, v198, v198
	v_max_f32_e32 v199, v199, v199
	v_max_f32_e32 v200, v200, v200
	v_max_f32_e32 v201, v201, v201
	v_max_f32_e32 v202, v202, v202
	v_max_f32_e32 v203, v203, v203
	v_med3_f32 v170, v170, s20, v13
	v_med3_f32 v171, v171, s20, v13
	v_med3_f32 v172, v172, s20, v13
	v_med3_f32 v173, v173, s20, v13
	v_med3_f32 v174, v174, s20, v13
	v_med3_f32 v175, v175, s20, v13
	v_med3_f32 v176, v176, s20, v13
	v_med3_f32 v177, v177, s20, v13
	v_med3_f32 v196, v196, s20, v13
	v_med3_f32 v197, v197, s20, v13
	v_med3_f32 v198, v198, s20, v13
	v_med3_f32 v199, v199, s20, v13
	v_med3_f32 v200, v200, s20, v13
	v_med3_f32 v201, v201, s20, v13
	v_med3_f32 v202, v202, s20, v13
	v_med3_f32 v203, v203, s20, v13
	v_mov_b32_e32 v208, 0
	v_mov_b32_e32 v209, 0
	v_mov_b32_e32 v210, 0
	v_mov_b32_e32 v211, 0
	v_cvt_pk_fp8_f32 v208, v170, v171
	v_cvt_pk_fp8_f32 v209, v174, v175
	v_cvt_pk_fp8_f32 v210, v196, v197
	v_cvt_pk_fp8_f32 v211, v200, v201
	v_cvt_pk_fp8_f32 v208, v172, v173 op_sel:[0,0,1]
	v_cvt_pk_fp8_f32 v209, v176, v177 op_sel:[0,0,1]
	v_cvt_pk_fp8_f32 v210, v198, v199 op_sel:[0,0,1]
	v_cvt_pk_fp8_f32 v211, v202, v203 op_sel:[0,0,1]
	s_nop 0
	global_store_dwordx4 v11, v[208:211], s[14:15]
	ds_read_b32 v170, v8
	ds_read_b32 v171, v8 offset:512
	ds_read_b32 v172, v8 offset:1024
	ds_read_b32 v173, v8 offset:1536
	ds_read_b32 v174, v8 offset:2048
	ds_read_b32 v175, v8 offset:2560
	ds_read_b32 v176, v8 offset:3072
	ds_read_b32 v177, v8 offset:3584
	ds_read_b32 v196, v8 offset:4096
	ds_read_b32 v197, v8 offset:4608
	ds_read_b32 v198, v8 offset:5120
	ds_read_b32 v199, v8 offset:5632
	ds_read_b32 v200, v8 offset:6144
	ds_read_b32 v201, v8 offset:6656
	ds_read_b32 v202, v8 offset:7168
	ds_read_b32 v203, v8 offset:7680
	s_waitcnt lgkmcnt(0)
	v_max_f32_e32 v170, v170, v170
	v_max_f32_e32 v171, v171, v171
	v_max_f32_e32 v172, v172, v172
	v_max_f32_e32 v173, v173, v173
	v_max_f32_e32 v174, v174, v174
	v_max_f32_e32 v175, v175, v175
	v_max_f32_e32 v176, v176, v176
	v_max_f32_e32 v177, v177, v177
	v_max_f32_e32 v196, v196, v196
	v_max_f32_e32 v197, v197, v197
	v_max_f32_e32 v198, v198, v198
	v_max_f32_e32 v199, v199, v199
	v_max_f32_e32 v200, v200, v200
	v_max_f32_e32 v201, v201, v201
	v_max_f32_e32 v202, v202, v202
	v_max_f32_e32 v203, v203, v203
	v_med3_f32 v170, v170, s20, v13
	v_med3_f32 v171, v171, s20, v13
	v_med3_f32 v172, v172, s20, v13
	v_med3_f32 v173, v173, s20, v13
	v_med3_f32 v174, v174, s20, v13
	v_med3_f32 v175, v175, s20, v13
	v_med3_f32 v176, v176, s20, v13
	v_med3_f32 v177, v177, s20, v13
	v_med3_f32 v196, v196, s20, v13
	v_med3_f32 v197, v197, s20, v13
	v_med3_f32 v198, v198, s20, v13
	v_med3_f32 v199, v199, s20, v13
	v_med3_f32 v200, v200, s20, v13
	v_med3_f32 v201, v201, s20, v13
	v_med3_f32 v202, v202, s20, v13
	v_med3_f32 v203, v203, s20, v13
	v_mov_b32_e32 v208, 0
	v_mov_b32_e32 v209, 0
	v_mov_b32_e32 v210, 0
	v_mov_b32_e32 v211, 0
	v_cvt_pk_fp8_f32 v208, v170, v171
	v_cvt_pk_fp8_f32 v209, v174, v175
	v_cvt_pk_fp8_f32 v210, v196, v197
	v_cvt_pk_fp8_f32 v211, v200, v201
	v_cvt_pk_fp8_f32 v208, v172, v173 op_sel:[0,0,1]
	v_cvt_pk_fp8_f32 v209, v176, v177 op_sel:[0,0,1]
	v_cvt_pk_fp8_f32 v210, v198, v199 op_sel:[0,0,1]
	v_cvt_pk_fp8_f32 v211, v202, v203 op_sel:[0,0,1]
	s_nop 0
	global_store_dwordx4 v12, v[208:211], s[14:15]
	s_waitcnt vmcnt(32)
	v_mul_f32_e32 v68, 0x43000000, v68
	v_mul_f32_e32 v69, 0x43000000, v69
	v_mul_f32_e32 v70, 0x43000000, v70
	v_mul_f32_e32 v71, 0x43000000, v71
	ds_write_b128 v5, v[68:71]
	v_mul_f32_e32 v72, 0x43000000, v72
	v_mul_f32_e32 v73, 0x43000000, v73
	v_mul_f32_e32 v74, 0x43000000, v74
	v_mul_f32_e32 v75, 0x43000000, v75
	ds_write_b128 v5, v[72:75] offset:1024
	v_mul_f32_e32 v76, 0x43000000, v76
	v_mul_f32_e32 v77, 0x43000000, v77
	v_mul_f32_e32 v78, 0x43000000, v78
	v_mul_f32_e32 v79, 0x43000000, v79
	ds_write_b128 v5, v[76:79] offset:2048
	v_mul_f32_e32 v80, 0x43000000, v80
	v_mul_f32_e32 v81, 0x43000000, v81
	v_mul_f32_e32 v82, 0x43000000, v82
	v_mul_f32_e32 v83, 0x43000000, v83
	ds_write_b128 v5, v[80:83] offset:3072
	v_mul_f32_e32 v84, 0x43000000, v84
	v_mul_f32_e32 v85, 0x43000000, v85
	v_mul_f32_e32 v86, 0x43000000, v86
	v_mul_f32_e32 v87, 0x43000000, v87
	ds_write_b128 v5, v[84:87] offset:4096
	v_mul_f32_e32 v88, 0x43000000, v88
	v_mul_f32_e32 v89, 0x43000000, v89
	v_mul_f32_e32 v90, 0x43000000, v90
	v_mul_f32_e32 v91, 0x43000000, v91
	ds_write_b128 v5, v[88:91] offset:5120
	v_mul_f32_e32 v92, 0x43000000, v92
	v_mul_f32_e32 v93, 0x43000000, v93
	v_mul_f32_e32 v94, 0x43000000, v94
	v_mul_f32_e32 v95, 0x43000000, v95
	ds_write_b128 v5, v[92:95] offset:6144
	v_mul_f32_e32 v96, 0x43000000, v96
	v_mul_f32_e32 v97, 0x43000000, v97
	v_mul_f32_e32 v98, 0x43000000, v98
	v_mul_f32_e32 v99, 0x43000000, v99
	ds_write_b128 v5, v[96:99] offset:7168
	s_waitcnt lgkmcnt(0)
	s_barrier
; #define GAS __attribute__((address_space(1)))
; #define LAS __attribute__((address_space(3)))
; #define LDS_WAIT() asm volatile("s_waitcnt lgkmcnt(0)" ::: "memory")
;     const int pr = item >> 1, kb = 2 * (pr / nblk) + (item & 1), nb = pr % nblk, k0 = 64 * kb, n0 = 32 * nb;
;     const int nr = n0 + (lane & 31); const int sc = MAP == 1 ? src_col_in(nr) : nr;
;     float v[32];
; #pragma unroll
;     for (int i = 0; i < 32; ++i) v[i] = sc >= 0 ? W[(size_t)(k0 + 2 * i + (lane >> 5)) * Nsrc + sc] : 0.f;
; #pragma unroll
;     for (int i = 0; i < 32; ++i) { const int k = k0 + 2 * i + (lane >> 5); float x = v[i] * wscale; if (KS) x *= (k < ksplit ? ksA[k] : ksB[k - ksplit]); scr[(2 * i + (lane >> 5)) * 33 + (lane & 31)] = x; }
;     LDS_WAIT(); asm volatile("" ::: "memory");
;     const int c = lane & 7;
; #pragma unroll
;     for (int j = 0; j < 4; ++j) { const int n = (lane >> 3) + 8 * j; const LAS float* s = scr + (8 * c) * 33 + n;
;         const unsigned long long o = (unsigned long long)pg8::pk4_fp8(s[0 * 33], s[1 * 33], s[2 * 33], s[3 * 33]) | ((unsigned long long)pg8::pk4_fp8(s[4 * 33], s[5 * 33], s[6 * 33], s[7 * 33]) << 32);
;         *(GAS unsigned long long*)(WT + (size_t)(n0 + n) * K + k0 + 8 * c) = o; }
;     LDS_WAIT(); asm volatile("" ::: "memory");
; }
; __global__ void __launch_bounds__(NWAVES * 64, 2) hybrid_fwd(Args args) {
;     ...
;             p0_transpose_item_f8<false>(args.in[16] + (size_t)l * FF * DM, FF, DM, DM / 32, (unsigned char*)(ws + WS_WDN + l * SZ_WDN), 128.f, args.in[16], args.in[16], 0, scr, r, lane);
	s_add_i32 s17, s16, 3168
	s_min_u32 s17, s17, 0xfff
	s_lshr_b32 s18, s17, 5
	s_add_i32 s18, s18, 0
	s_and_b32 s19, s17, 31
	s_lshl_b32 s18, s18, 21
	s_lshl_b32 s19, s19, 9
	s_add_u32 s18, s18, s19
	s_add_u32 s12, s2, s18
	s_addc_u32 s13, s3, 0
	global_load_dwordx4 v[68:71], v10, s[12:13]
	s_add_u32 s12, s12, 0x8000
	s_addc_u32 s13, s13, 0
	global_load_dwordx4 v[72:75], v10, s[12:13]
	s_add_u32 s12, s12, 0x8000
	s_addc_u32 s13, s13, 0
	global_load_dwordx4 v[76:79], v10, s[12:13]
	s_add_u32 s12, s12, 0x8000
	s_addc_u32 s13, s13, 0
	global_load_dwordx4 v[80:83], v10, s[12:13]
	s_add_u32 s12, s12, 0x8000
	s_addc_u32 s13, s13, 0
	global_load_dwordx4 v[84:87], v10, s[12:13]
	s_add_u32 s12, s12, 0x8000
	s_addc_u32 s13, s13, 0
	global_load_dwordx4 v[88:91], v10, s[12:13]
	s_add_u32 s12, s12, 0x8000
	s_addc_u32 s13, s13, 0
	global_load_dwordx4 v[92:95], v10, s[12:13]
	s_add_u32 s12, s12, 0x8000
	s_addc_u32 s13, s13, 0
	global_load_dwordx4 v[96:99], v10, s[12:13]
	s_add_i32 s17, s16, 2784
	s_min_u32 s17, s17, 0xfff
	s_lshr_b32 s18, s17, 5
	s_add_i32 s18, s18, 0
	s_and_b32 s19, s17, 31
	s_lshl_b32 s19, s19, 21
	s_lshl_b32 s18, s18, 7
	s_add_u32 s18, s18, s19
	s_add_u32 s14, s4, s18
	s_addc_u32 s15, s5, 0
	ds_read_b32 v170, v7
	ds_read_b32 v171, v7 offset:512
	ds_read_b32 v172, v7 offset:1024
	ds_read_b32 v173, v7 offset:1536
	ds_read_b32 v174, v7 offset:2048
	ds_read_b32 v175, v7 offset:2560
	ds_read_b32 v176, v7 offset:3072
	ds_read_b32 v177, v7 offset:3584
	ds_read_b32 v196, v7 offset:4096
	ds_read_b32 v197, v7 offset:4608
	ds_read_b32 v198, v7 offset:5120
	ds_read_b32 v199, v7 offset:5632
	ds_read_b32 v200, v7 offset:6144
	ds_read_b32 v201, v7 offset:6656
	ds_read_b32 v202, v7 offset:7168
	ds_read_b32 v203, v7 offset:7680
	s_waitcnt lgkmcnt(0)
	v_max_f32_e32 v170, v170, v170
	v_max_f32_e32 v171, v171, v171
	v_max_f32_e32 v172, v172, v172
	v_max_f32_e32 v173, v173, v173
	v_max_f32_e32 v174, v174, v174
	v_max_f32_e32 v175, v175, v175
	v_max_f32_e32 v176, v176, v176
	v_max_f32_e32 v177, v177, v177
	v_max_f32_e32 v196, v196, v196
	v_max_f32_e32 v197, v197, v197
	v_max_f32_e32 v198, v198, v198
	v_max_f32_e32 v199, v199, v199
	v_max_f32_e32 v200, v200, v200
	v_max_f32_e32 v201, v201, v201
	v_max_f32_e32 v202, v202, v202
	v_max_f32_e32 v203, v203, v203
	v_med3_f32 v170, v170, s20, v13
	v_med3_f32 v171, v171, s20, v13
	v_med3_f32 v172, v172, s20, v13
	v_med3_f32 v173, v173, s20, v13
	v_med3_f32 v174, v174, s20, v13
	v_med3_f32 v175, v175, s20, v13
	v_med3_f32 v176, v176, s20, v13
	v_med3_f32 v177, v177, s20, v13
	v_med3_f32 v196, v196, s20, v13
	v_med3_f32 v197, v197, s20, v13
	v_med3_f32 v198, v198, s20, v13
	v_med3_f32 v199, v199, s20, v13
	v_med3_f32 v200, v200, s20, v13
	v_med3_f32 v201, v201, s20, v13
	v_med3_f32 v202, v202, s20, v13
	v_med3_f32 v203, v203, s20, v13
	v_mov_b32_e32 v208, 0
	v_mov_b32_e32 v209, 0
	v_mov_b32_e32 v210, 0
	v_mov_b32_e32 v211, 0
	v_cvt_pk_fp8_f32 v208, v170, v171
	v_cvt_pk_fp8_f32 v209, v174, v175
	v_cvt_pk_fp8_f32 v210, v196, v197
	v_cvt_pk_fp8_f32 v211, v200, v201
	v_cvt_pk_fp8_f32 v208, v172, v173 op_sel:[0,0,1]
	v_cvt_pk_fp8_f32 v209, v176, v177 op_sel:[0,0,1]
	v_cvt_pk_fp8_f32 v210, v198, v199 op_sel:[0,0,1]
	v_cvt_pk_fp8_f32 v211, v202, v203 op_sel:[0,0,1]
	s_nop 0
	global_store_dwordx4 v11, v[208:211], s[14:15]
	ds_read_b32 v170, v9
	ds_read_b32 v171, v9 offset:512
	ds_read_b32 v172, v9 offset:1024
	ds_read_b32 v173, v9 offset:1536
	ds_read_b32 v174, v9 offset:2048
	ds_read_b32 v175, v9 offset:2560
	ds_read_b32 v176, v9 offset:3072
	ds_read_b32 v177, v9 offset:3584
	ds_read_b32 v196, v9 offset:4096
	ds_read_b32 v197, v9 offset:4608
	ds_read_b32 v198, v9 offset:5120
	ds_read_b32 v199, v9 offset:5632
	ds_read_b32 v200, v9 offset:6144
	ds_read_b32 v201, v9 offset:6656
	ds_read_b32 v202, v9 offset:7168
	ds_read_b32 v203, v9 offset:7680
	s_waitcnt lgkmcnt(0)
	v_max_f32_e32 v170, v170, v170
	v_max_f32_e32 v171, v171, v171
	v_max_f32_e32 v172, v172, v172
	v_max_f32_e32 v173, v173, v173
	v_max_f32_e32 v174, v174, v174
	v_max_f32_e32 v175, v175, v175
	v_max_f32_e32 v176, v176, v176
	v_max_f32_e32 v177, v177, v177
	v_max_f32_e32 v196, v196, v196
	v_max_f32_e32 v197, v197, v197
	v_max_f32_e32 v198, v198, v198
	v_max_f32_e32 v199, v199, v199
	v_max_f32_e32 v200, v200, v200
	v_max_f32_e32 v201, v201, v201
	v_max_f32_e32 v202, v202, v202
	v_max_f32_e32 v203, v203, v203
	v_med3_f32 v170, v170, s20, v13
	v_med3_f32 v171, v171, s20, v13
	v_med3_f32 v172, v172, s20, v13
	v_med3_f32 v173, v173, s20, v13
	v_med3_f32 v174, v174, s20, v13
	v_med3_f32 v175, v175, s20, v13
	v_med3_f32 v176, v176, s20, v13
	v_med3_f32 v177, v177, s20, v13
	v_med3_f32 v196, v196, s20, v13
	v_med3_f32 v197, v197, s20, v13
	v_med3_f32 v198, v198, s20, v13
	v_med3_f32 v199, v199, s20, v13
	v_med3_f32 v200, v200, s20, v13
	v_med3_f32 v201, v201, s20, v13
	v_med3_f32 v202, v202, s20, v13
	v_med3_f32 v203, v203, s20, v13
	v_mov_b32_e32 v208, 0
	v_mov_b32_e32 v209, 0
	v_mov_b32_e32 v210, 0
	v_mov_b32_e32 v211, 0
	v_cvt_pk_fp8_f32 v208, v170, v171
	v_cvt_pk_fp8_f32 v209, v174, v175
	v_cvt_pk_fp8_f32 v210, v196, v197
	v_cvt_pk_fp8_f32 v211, v200, v201
	v_cvt_pk_fp8_f32 v208, v172, v173 op_sel:[0,0,1]
	v_cvt_pk_fp8_f32 v209, v176, v177 op_sel:[0,0,1]
	v_cvt_pk_fp8_f32 v210, v198, v199 op_sel:[0,0,1]
	v_cvt_pk_fp8_f32 v211, v202, v203 op_sel:[0,0,1]
	s_nop 0
	global_store_dwordx4 v12, v[208:211], s[14:15]
	s_waitcnt vmcnt(32)
	v_mul_f32_e32 v100, 0x43000000, v100
	v_mul_f32_e32 v101, 0x43000000, v101
	v_mul_f32_e32 v102, 0x43000000, v102
	v_mul_f32_e32 v103, 0x43000000, v103
	ds_write_b128 v4, v[100:103]
	v_mul_f32_e32 v104, 0x43000000, v104
	v_mul_f32_e32 v105, 0x43000000, v105
	v_mul_f32_e32 v106, 0x43000000, v106
	v_mul_f32_e32 v107, 0x43000000, v107
	ds_write_b128 v4, v[104:107] offset:1024
	v_mul_f32_e32 v108, 0x43000000, v108
	v_mul_f32_e32 v109, 0x43000000, v109
	v_mul_f32_e32 v110, 0x43000000, v110
	v_mul_f32_e32 v111, 0x43000000, v111
	ds_write_b128 v4, v[108:111] offset:2048
	v_mul_f32_e32 v112, 0x43000000, v112
	v_mul_f32_e32 v113, 0x43000000, v113
	v_mul_f32_e32 v114, 0x43000000, v114
	v_mul_f32_e32 v115, 0x43000000, v115
	ds_write_b128 v4, v[112:115] offset:3072
	v_mul_f32_e32 v116, 0x43000000, v116
	v_mul_f32_e32 v117, 0x43000000, v117
	v_mul_f32_e32 v118, 0x43000000, v118
	v_mul_f32_e32 v119, 0x43000000, v119
	ds_write_b128 v4, v[116:119] offset:4096
	v_mul_f32_e32 v120, 0x43000000, v120
	v_mul_f32_e32 v121, 0x43000000, v121
	v_mul_f32_e32 v122, 0x43000000, v122
	v_mul_f32_e32 v123, 0x43000000, v123
	ds_write_b128 v4, v[120:123] offset:5120
	v_mul_f32_e32 v124, 0x43000000, v124
	v_mul_f32_e32 v125, 0x43000000, v125
	v_mul_f32_e32 v126, 0x43000000, v126
	v_mul_f32_e32 v127, 0x43000000, v127
	ds_write_b128 v4, v[124:127] offset:6144
	v_mul_f32_e32 v128, 0x43000000, v128
	v_mul_f32_e32 v129, 0x43000000, v129
	v_mul_f32_e32 v130, 0x43000000, v130
	v_mul_f32_e32 v131, 0x43000000, v131
	ds_write_b128 v4, v[128:131] offset:7168
	s_waitcnt lgkmcnt(0)
	s_barrier
; #define GAS __attribute__((address_space(1)))
; #define LAS __attribute__((address_space(3)))
; #define LDS_WAIT() asm volatile("s_waitcnt lgkmcnt(0)" ::: "memory")
;     const int pr = item >> 1, kb = 2 * (pr / nblk) + (item & 1), nb = pr % nblk, k0 = 64 * kb, n0 = 32 * nb;
;     const int nr = n0 + (lane & 31); const int sc = MAP == 1 ? src_col_in(nr) : nr;
;     float v[32];
; #pragma unroll
;     for (int i = 0; i < 32; ++i) v[i] = sc >= 0 ? W[(size_t)(k0 + 2 * i + (lane >> 5)) * Nsrc + sc] : 0.f;
; #pragma unroll
;     for (int i = 0; i < 32; ++i) { const int k = k0 + 2 * i + (lane >> 5); float x = v[i] * wscale; if (KS) x *= (k < ksplit ? ksA[k] : ksB[k - ksplit]); scr[(2 * i + (lane >> 5)) * 33 + (lane & 31)] = x; }
;     LDS_WAIT(); asm volatile("" ::: "memory");
;     const int c = lane & 7;
; #pragma unroll
;     for (int j = 0; j < 4; ++j) { const int n = (lane >> 3) + 8 * j; const LAS float* s = scr + (8 * c) * 33 + n;
;         const unsigned long long o = (unsigned long long)pg8::pk4_fp8(s[0 * 33], s[1 * 33], s[2 * 33], s[3 * 33]) | ((unsigned long long)pg8::pk4_fp8(s[4 * 33], s[5 * 33], s[6 * 33], s[7 * 33]) << 32);
;         *(GAS unsigned long long*)(WT + (size_t)(n0 + n) * K + k0 + 8 * c) = o; }
;     LDS_WAIT(); asm volatile("" ::: "memory");
; }
; __global__ void __launch_bounds__(NWAVES * 64, 2) hybrid_fwd(Args args) {
;     ...
;             p0_transpose_item_f8<false>(args.in[16] + (size_t)l * FF * DM, FF, DM, DM / 32, (unsigned char*)(ws + WS_WDN + l * SZ_WDN), 128.f, args.in[16], args.in[16], 0, scr, r, lane);
	s_add_i32 s17, s16, 3264
	s_min_u32 s17, s17, 0xfff
	s_lshr_b32 s18, s17, 5
	s_add_i32 s18, s18, 0
	s_and_b32 s19, s17, 31
	s_lshl_b32 s18, s18, 21
	s_lshl_b32 s19, s19, 9
	s_add_u32 s18, s18, s19
	s_add_u32 s12, s2, s18
	s_addc_u32 s13, s3, 0
	global_load_dwordx4 v[100:103], v10, s[12:13]
	s_add_u32 s12, s12, 0x8000
	s_addc_u32 s13, s13, 0
	global_load_dwordx4 v[104:107], v10, s[12:13]
	s_add_u32 s12, s12, 0x8000
	s_addc_u32 s13, s13, 0
	global_load_dwordx4 v[108:111], v10, s[12:13]
	s_add_u32 s12, s12, 0x8000
	s_addc_u32 s13, s13, 0
	global_load_dwordx4 v[112:115], v10, s[12:13]
	s_add_u32 s12, s12, 0x8000
	s_addc_u32 s13, s13, 0
	global_load_dwordx4 v[116:119], v10, s[12:13]
	s_add_u32 s12, s12, 0x8000
	s_addc_u32 s13, s13, 0
	global_load_dwordx4 v[120:123], v10, s[12:13]
	s_add_u32 s12, s12, 0x8000
	s_addc_u32 s13, s13, 0
	global_load_dwordx4 v[124:127], v10, s[12:13]
	s_add_u32 s12, s12, 0x8000
	s_addc_u32 s13, s13, 0
	global_load_dwordx4 v[128:131], v10, s[12:13]
	s_add_i32 s17, s16, 2880
	s_min_u32 s17, s17, 0xfff
	s_lshr_b32 s18, s17, 5
	s_add_i32 s18, s18, 0
	s_and_b32 s19, s17, 31
	s_lshl_b32 s19, s19, 21
	s_lshl_b32 s18, s18, 7
	s_add_u32 s18, s18, s19
	s_add_u32 s14, s4, s18
	s_addc_u32 s15, s5, 0
	ds_read_b32 v170, v6
	ds_read_b32 v171, v6 offset:512
	ds_read_b32 v172, v6 offset:1024
	ds_read_b32 v173, v6 offset:1536
	ds_read_b32 v174, v6 offset:2048
	ds_read_b32 v175, v6 offset:2560
	ds_read_b32 v176, v6 offset:3072
	ds_read_b32 v177, v6 offset:3584
	ds_read_b32 v196, v6 offset:4096
	ds_read_b32 v197, v6 offset:4608
	ds_read_b32 v198, v6 offset:5120
	ds_read_b32 v199, v6 offset:5632
	ds_read_b32 v200, v6 offset:6144
	ds_read_b32 v201, v6 offset:6656
	ds_read_b32 v202, v6 offset:7168
	ds_read_b32 v203, v6 offset:7680
	s_waitcnt lgkmcnt(0)
	v_max_f32_e32 v170, v170, v170
	v_max_f32_e32 v171, v171, v171
	v_max_f32_e32 v172, v172, v172
	v_max_f32_e32 v173, v173, v173
	v_max_f32_e32 v174, v174, v174
	v_max_f32_e32 v175, v175, v175
	v_max_f32_e32 v176, v176, v176
	v_max_f32_e32 v177, v177, v177
	v_max_f32_e32 v196, v196, v196
	v_max_f32_e32 v197, v197, v197
	v_max_f32_e32 v198, v198, v198
	v_max_f32_e32 v199, v199, v199
	v_max_f32_e32 v200, v200, v200
	v_max_f32_e32 v201, v201, v201
	v_max_f32_e32 v202, v202, v202
	v_max_f32_e32 v203, v203, v203
	v_med3_f32 v170, v170, s20, v13
	v_med3_f32 v171, v171, s20, v13
	v_med3_f32 v172, v172, s20, v13
	v_med3_f32 v173, v173, s20, v13
	v_med3_f32 v174, v174, s20, v13
	v_med3_f32 v175, v175, s20, v13
	v_med3_f32 v176, v176, s20, v13
	v_med3_f32 v177, v177, s20, v13
	v_med3_f32 v196, v196, s20, v13
	v_med3_f32 v197, v197, s20, v13
	v_med3_f32 v198, v198, s20, v13
	v_med3_f32 v199, v199, s20, v13
	v_med3_f32 v200, v200, s20, v13
	v_med3_f32 v201, v201, s20, v13
	v_med3_f32 v202, v202, s20, v13
	v_med3_f32 v203, v203, s20, v13
	v_mov_b32_e32 v208, 0
	v_mov_b32_e32 v209, 0
	v_mov_b32_e32 v210, 0
	v_mov_b32_e32 v211, 0
	v_cvt_pk_fp8_f32 v208, v170, v171
	v_cvt_pk_fp8_f32 v209, v174, v175
	v_cvt_pk_fp8_f32 v210, v196, v197
	v_cvt_pk_fp8_f32 v211, v200, v201
	v_cvt_pk_fp8_f32 v208, v172, v173 op_sel:[0,0,1]
	v_cvt_pk_fp8_f32 v209, v176, v177 op_sel:[0,0,1]
	v_cvt_pk_fp8_f32 v210, v198, v199 op_sel:[0,0,1]
	v_cvt_pk_fp8_f32 v211, v202, v203 op_sel:[0,0,1]
	s_nop 0
	global_store_dwordx4 v11, v[208:211], s[14:15]
	ds_read_b32 v170, v8
	ds_read_b32 v171, v8 offset:512
	ds_read_b32 v172, v8 offset:1024
	ds_read_b32 v173, v8 offset:1536
	ds_read_b32 v174, v8 offset:2048
	ds_read_b32 v175, v8 offset:2560
	ds_read_b32 v176, v8 offset:3072
	ds_read_b32 v177, v8 offset:3584
	ds_read_b32 v196, v8 offset:4096
	ds_read_b32 v197, v8 offset:4608
	ds_read_b32 v198, v8 offset:5120
	ds_read_b32 v199, v8 offset:5632
	ds_read_b32 v200, v8 offset:6144
	ds_read_b32 v201, v8 offset:6656
	ds_read_b32 v202, v8 offset:7168
	ds_read_b32 v203, v8 offset:7680
	s_waitcnt lgkmcnt(0)
	v_max_f32_e32 v170, v170, v170
	v_max_f32_e32 v171, v171, v171
	v_max_f32_e32 v172, v172, v172
	v_max_f32_e32 v173, v173, v173
	v_max_f32_e32 v174, v174, v174
	v_max_f32_e32 v175, v175, v175
	v_max_f32_e32 v176, v176, v176
	v_max_f32_e32 v177, v177, v177
	v_max_f32_e32 v196, v196, v196
	v_max_f32_e32 v197, v197, v197
	v_max_f32_e32 v198, v198, v198
	v_max_f32_e32 v199, v199, v199
	v_max_f32_e32 v200, v200, v200
	v_max_f32_e32 v201, v201, v201
	v_max_f32_e32 v202, v202, v202
	v_max_f32_e32 v203, v203, v203
	v_med3_f32 v170, v170, s20, v13
	v_med3_f32 v171, v171, s20, v13
	v_med3_f32 v172, v172, s20, v13
	v_med3_f32 v173, v173, s20, v13
	v_med3_f32 v174, v174, s20, v13
	v_med3_f32 v175, v175, s20, v13
	v_med3_f32 v176, v176, s20, v13
	v_med3_f32 v177, v177, s20, v13
	v_med3_f32 v196, v196, s20, v13
	v_med3_f32 v197, v197, s20, v13
	v_med3_f32 v198, v198, s20, v13
	v_med3_f32 v199, v199, s20, v13
	v_med3_f32 v200, v200, s20, v13
	v_med3_f32 v201, v201, s20, v13
	v_med3_f32 v202, v202, s20, v13
	v_med3_f32 v203, v203, s20, v13
	v_mov_b32_e32 v208, 0
	v_mov_b32_e32 v209, 0
	v_mov_b32_e32 v210, 0
	v_mov_b32_e32 v211, 0
	v_cvt_pk_fp8_f32 v208, v170, v171
	v_cvt_pk_fp8_f32 v209, v174, v175
	v_cvt_pk_fp8_f32 v210, v196, v197
	v_cvt_pk_fp8_f32 v211, v200, v201
	v_cvt_pk_fp8_f32 v208, v172, v173 op_sel:[0,0,1]
	v_cvt_pk_fp8_f32 v209, v176, v177 op_sel:[0,0,1]
	v_cvt_pk_fp8_f32 v210, v198, v199 op_sel:[0,0,1]
	v_cvt_pk_fp8_f32 v211, v202, v203 op_sel:[0,0,1]
	s_nop 0
	global_store_dwordx4 v12, v[208:211], s[14:15]
	s_waitcnt vmcnt(32)
	v_mul_f32_e32 v132, 0x43000000, v132
	v_mul_f32_e32 v133, 0x43000000, v133
	v_mul_f32_e32 v134, 0x43000000, v134
	v_mul_f32_e32 v135, 0x43000000, v135
	ds_write_b128 v5, v[132:135]
	v_mul_f32_e32 v136, 0x43000000, v136
	v_mul_f32_e32 v137, 0x43000000, v137
	v_mul_f32_e32 v138, 0x43000000, v138
	v_mul_f32_e32 v139, 0x43000000, v139
	ds_write_b128 v5, v[136:139] offset:1024
	v_mul_f32_e32 v140, 0x43000000, v140
	v_mul_f32_e32 v141, 0x43000000, v141
	v_mul_f32_e32 v142, 0x43000000, v142
	v_mul_f32_e32 v143, 0x43000000, v143
	ds_write_b128 v5, v[140:143] offset:2048
	v_mul_f32_e32 v144, 0x43000000, v144
	v_mul_f32_e32 v145, 0x43000000, v145
	v_mul_f32_e32 v146, 0x43000000, v146
	v_mul_f32_e32 v147, 0x43000000, v147
	ds_write_b128 v5, v[144:147] offset:3072
	v_mul_f32_e32 v148, 0x43000000, v148
	v_mul_f32_e32 v149, 0x43000000, v149
	v_mul_f32_e32 v150, 0x43000000, v150
	v_mul_f32_e32 v151, 0x43000000, v151
	ds_write_b128 v5, v[148:151] offset:4096
	v_mul_f32_e32 v152, 0x43000000, v152
	v_mul_f32_e32 v153, 0x43000000, v153
	v_mul_f32_e32 v154, 0x43000000, v154
	v_mul_f32_e32 v155, 0x43000000, v155
	ds_write_b128 v5, v[152:155] offset:5120
	v_mul_f32_e32 v156, 0x43000000, v156
	v_mul_f32_e32 v157, 0x43000000, v157
	v_mul_f32_e32 v158, 0x43000000, v158
	v_mul_f32_e32 v159, 0x43000000, v159
	ds_write_b128 v5, v[156:159] offset:6144
	v_mul_f32_e32 v160, 0x43000000, v160
	v_mul_f32_e32 v161, 0x43000000, v161
	v_mul_f32_e32 v162, 0x43000000, v162
	v_mul_f32_e32 v163, 0x43000000, v163
	ds_write_b128 v5, v[160:163] offset:7168
	s_waitcnt lgkmcnt(0)
	s_barrier
; #define GAS __attribute__((address_space(1)))
; #define LAS __attribute__((address_space(3)))
; #define LDS_WAIT() asm volatile("s_waitcnt lgkmcnt(0)" ::: "memory")
;     const int pr = item >> 1, kb = 2 * (pr / nblk) + (item & 1), nb = pr % nblk, k0 = 64 * kb, n0 = 32 * nb;
;     const int nr = n0 + (lane & 31); const int sc = MAP == 1 ? src_col_in(nr) : nr;
;     float v[32];
; #pragma unroll
;     for (int i = 0; i < 32; ++i) v[i] = sc >= 0 ? W[(size_t)(k0 + 2 * i + (lane >> 5)) * Nsrc + sc] : 0.f;
; #pragma unroll
;     for (int i = 0; i < 32; ++i) { const int k = k0 + 2 * i + (lane >> 5); float x = v[i] * wscale; if (KS) x *= (k < ksplit ? ksA[k] : ksB[k - ksplit]); scr[(2 * i + (lane >> 5)) * 33 + (lane & 31)] = x; }
;     LDS_WAIT(); asm volatile("" ::: "memory");
;     const int c = lane & 7;
; #pragma unroll
;     for (int j = 0; j < 4; ++j) { const int n = (lane >> 3) + 8 * j; const LAS float* s = scr + (8 * c) * 33 + n;
;         const unsigned long long o = (unsigned long long)pg8::pk4_fp8(s[0 * 33], s[1 * 33], s[2 * 33], s[3 * 33]) | ((unsigned long long)pg8::pk4_fp8(s[4 * 33], s[5 * 33], s[6 * 33], s[7 * 33]) << 32);
;         *(GAS unsigned long long*)(WT + (size_t)(n0 + n) * K + k0 + 8 * c) = o; }
;     LDS_WAIT(); asm volatile("" ::: "memory");
; }
; __global__ void __launch_bounds__(NWAVES * 64, 2) hybrid_fwd(Args args) {
;     ...
;             p0_transpose_item_f8<false>(args.in[16] + (size_t)l * FF * DM, FF, DM, DM / 32, (unsigned char*)(ws + WS_WDN + l * SZ_WDN), 128.f, args.in[16], args.in[16], 0, scr, r, lane);
	s_add_i32 s17, s16, 3360
	s_min_u32 s17, s17, 0xfff
	s_lshr_b32 s18, s17, 5
	s_add_i32 s18, s18, 0
	s_and_b32 s19, s17, 31
	s_lshl_b32 s18, s18, 21
	s_lshl_b32 s19, s19, 9
	s_add_u32 s18, s18, s19
	s_add_u32 s12, s2, s18
	s_addc_u32 s13, s3, 0
	global_load_dwordx4 v[132:135], v10, s[12:13]
	s_add_u32 s12, s12, 0x8000
	s_addc_u32 s13, s13, 0
	global_load_dwordx4 v[136:139], v10, s[12:13]
	s_add_u32 s12, s12, 0x8000
	s_addc_u32 s13, s13, 0
	global_load_dwordx4 v[140:143], v10, s[12:13]
	s_add_u32 s12, s12, 0x8000
	s_addc_u32 s13, s13, 0
	global_load_dwordx4 v[144:147], v10, s[12:13]
	s_add_u32 s12, s12, 0x8000
	s_addc_u32 s13, s13, 0
	global_load_dwordx4 v[148:151], v10, s[12:13]
	s_add_u32 s12, s12, 0x8000
	s_addc_u32 s13, s13, 0
	global_load_dwordx4 v[152:155], v10, s[12:13]
	s_add_u32 s12, s12, 0x8000
	s_addc_u32 s13, s13, 0
	global_load_dwordx4 v[156:159], v10, s[12:13]
	s_add_u32 s12, s12, 0x8000
	s_addc_u32 s13, s13, 0
	global_load_dwordx4 v[160:163], v10, s[12:13]
	s_add_i32 s17, s16, 2976
	s_min_u32 s17, s17, 0xfff
	s_lshr_b32 s18, s17, 5
	s_add_i32 s18, s18, 0
	s_and_b32 s19, s17, 31
	s_lshl_b32 s19, s19, 21
	s_lshl_b32 s18, s18, 7
	s_add_u32 s18, s18, s19
	s_add_u32 s14, s4, s18
	s_addc_u32 s15, s5, 0
	ds_read_b32 v170, v7
	ds_read_b32 v171, v7 offset:512
	ds_read_b32 v172, v7 offset:1024
	ds_read_b32 v173, v7 offset:1536
	ds_read_b32 v174, v7 offset:2048
	ds_read_b32 v175, v7 offset:2560
	ds_read_b32 v176, v7 offset:3072
	ds_read_b32 v177, v7 offset:3584
	ds_read_b32 v196, v7 offset:4096
	ds_read_b32 v197, v7 offset:4608
	ds_read_b32 v198, v7 offset:5120
	ds_read_b32 v199, v7 offset:5632
	ds_read_b32 v200, v7 offset:6144
	ds_read_b32 v201, v7 offset:6656
	ds_read_b32 v202, v7 offset:7168
	ds_read_b32 v203, v7 offset:7680
	s_waitcnt lgkmcnt(0)
	v_max_f32_e32 v170, v170, v170
	v_max_f32_e32 v171, v171, v171
	v_max_f32_e32 v172, v172, v172
	v_max_f32_e32 v173, v173, v173
	v_max_f32_e32 v174, v174, v174
	v_max_f32_e32 v175, v175, v175
	v_max_f32_e32 v176, v176, v176
	v_max_f32_e32 v177, v177, v177
	v_max_f32_e32 v196, v196, v196
	v_max_f32_e32 v197, v197, v197
	v_max_f32_e32 v198, v198, v198
	v_max_f32_e32 v199, v199, v199
	v_max_f32_e32 v200, v200, v200
	v_max_f32_e32 v201, v201, v201
	v_max_f32_e32 v202, v202, v202
	v_max_f32_e32 v203, v203, v203
	v_med3_f32 v170, v170, s20, v13
	v_med3_f32 v171, v171, s20, v13
	v_med3_f32 v172, v172, s20, v13
	v_med3_f32 v173, v173, s20, v13
	v_med3_f32 v174, v174, s20, v13
	v_med3_f32 v175, v175, s20, v13
	v_med3_f32 v176, v176, s20, v13
	v_med3_f32 v177, v177, s20, v13
	v_med3_f32 v196, v196, s20, v13
	v_med3_f32 v197, v197, s20, v13
	v_med3_f32 v198, v198, s20, v13
	v_med3_f32 v199, v199, s20, v13
	v_med3_f32 v200, v200, s20, v13
	v_med3_f32 v201, v201, s20, v13
	v_med3_f32 v202, v202, s20, v13
	v_med3_f32 v203, v203, s20, v13
	v_mov_b32_e32 v208, 0
	v_mov_b32_e32 v209, 0
	v_mov_b32_e32 v210, 0
	v_mov_b32_e32 v211, 0
	v_cvt_pk_fp8_f32 v208, v170, v171
	v_cvt_pk_fp8_f32 v209, v174, v175
	v_cvt_pk_fp8_f32 v210, v196, v197
	v_cvt_pk_fp8_f32 v211, v200, v201
	v_cvt_pk_fp8_f32 v208, v172, v173 op_sel:[0,0,1]
	v_cvt_pk_fp8_f32 v209, v176, v177 op_sel:[0,0,1]
	v_cvt_pk_fp8_f32 v210, v198, v199 op_sel:[0,0,1]
	v_cvt_pk_fp8_f32 v211, v202, v203 op_sel:[0,0,1]
	s_nop 0
	global_store_dwordx4 v11, v[208:211], s[14:15]
	ds_read_b32 v170, v9
	ds_read_b32 v171, v9 offset:512
	ds_read_b32 v172, v9 offset:1024
	ds_read_b32 v173, v9 offset:1536
	ds_read_b32 v174, v9 offset:2048
	ds_read_b32 v175, v9 offset:2560
	ds_read_b32 v176, v9 offset:3072
	ds_read_b32 v177, v9 offset:3584
	ds_read_b32 v196, v9 offset:4096
	ds_read_b32 v197, v9 offset:4608
	ds_read_b32 v198, v9 offset:5120
	ds_read_b32 v199, v9 offset:5632
	ds_read_b32 v200, v9 offset:6144
	ds_read_b32 v201, v9 offset:6656
	ds_read_b32 v202, v9 offset:7168
	ds_read_b32 v203, v9 offset:7680
	s_waitcnt lgkmcnt(0)
	v_max_f32_e32 v170, v170, v170
	v_max_f32_e32 v171, v171, v171
	v_max_f32_e32 v172, v172, v172
	v_max_f32_e32 v173, v173, v173
	v_max_f32_e32 v174, v174, v174
	v_max_f32_e32 v175, v175, v175
	v_max_f32_e32 v176, v176, v176
	v_max_f32_e32 v177, v177, v177
	v_max_f32_e32 v196, v196, v196
	v_max_f32_e32 v197, v197, v197
	v_max_f32_e32 v198, v198, v198
	v_max_f32_e32 v199, v199, v199
	v_max_f32_e32 v200, v200, v200
	v_max_f32_e32 v201, v201, v201
	v_max_f32_e32 v202, v202, v202
	v_max_f32_e32 v203, v203, v203
	v_med3_f32 v170, v170, s20, v13
	v_med3_f32 v171, v171, s20, v13
	v_med3_f32 v172, v172, s20, v13
	v_med3_f32 v173, v173, s20, v13
	v_med3_f32 v174, v174, s20, v13
	v_med3_f32 v175, v175, s20, v13
	v_med3_f32 v176, v176, s20, v13
	v_med3_f32 v177, v177, s20, v13
	v_med3_f32 v196, v196, s20, v13
	v_med3_f32 v197, v197, s20, v13
	v_med3_f32 v198, v198, s20, v13
	v_med3_f32 v199, v199, s20, v13
	v_med3_f32 v200, v200, s20, v13
	v_med3_f32 v201, v201, s20, v13
	v_med3_f32 v202, v202, s20, v13
	v_med3_f32 v203, v203, s20, v13
	v_mov_b32_e32 v208, 0
	v_mov_b32_e32 v209, 0
	v_mov_b32_e32 v210, 0
	v_mov_b32_e32 v211, 0
	v_cvt_pk_fp8_f32 v208, v170, v171
	v_cvt_pk_fp8_f32 v209, v174, v175
	v_cvt_pk_fp8_f32 v210, v196, v197
	v_cvt_pk_fp8_f32 v211, v200, v201
	v_cvt_pk_fp8_f32 v208, v172, v173 op_sel:[0,0,1]
	v_cvt_pk_fp8_f32 v209, v176, v177 op_sel:[0,0,1]
	v_cvt_pk_fp8_f32 v210, v198, v199 op_sel:[0,0,1]
	v_cvt_pk_fp8_f32 v211, v202, v203 op_sel:[0,0,1]
	s_nop 0
	global_store_dwordx4 v12, v[208:211], s[14:15]
	s_waitcnt vmcnt(32)
	v_mul_f32_e32 v36, 0x43000000, v36
	v_mul_f32_e32 v37, 0x43000000, v37
	v_mul_f32_e32 v38, 0x43000000, v38
	v_mul_f32_e32 v39, 0x43000000, v39
	ds_write_b128 v4, v[36:39]
	v_mul_f32_e32 v40, 0x43000000, v40
	v_mul_f32_e32 v41, 0x43000000, v41
	v_mul_f32_e32 v42, 0x43000000, v42
	v_mul_f32_e32 v43, 0x43000000, v43
	ds_write_b128 v4, v[40:43] offset:1024
	v_mul_f32_e32 v44, 0x43000000, v44
	v_mul_f32_e32 v45, 0x43000000, v45
	v_mul_f32_e32 v46, 0x43000000, v46
	v_mul_f32_e32 v47, 0x43000000, v47
	ds_write_b128 v4, v[44:47] offset:2048
	v_mul_f32_e32 v48, 0x43000000, v48
	v_mul_f32_e32 v49, 0x43000000, v49
	v_mul_f32_e32 v50, 0x43000000, v50
	v_mul_f32_e32 v51, 0x43000000, v51
	ds_write_b128 v4, v[48:51] offset:3072
	v_mul_f32_e32 v52, 0x43000000, v52
	v_mul_f32_e32 v53, 0x43000000, v53
	v_mul_f32_e32 v54, 0x43000000, v54
	v_mul_f32_e32 v55, 0x43000000, v55
	ds_write_b128 v4, v[52:55] offset:4096
	v_mul_f32_e32 v56, 0x43000000, v56
	v_mul_f32_e32 v57, 0x43000000, v57
	v_mul_f32_e32 v58, 0x43000000, v58
	v_mul_f32_e32 v59, 0x43000000, v59
	ds_write_b128 v4, v[56:59] offset:5120
	v_mul_f32_e32 v60, 0x43000000, v60
	v_mul_f32_e32 v61, 0x43000000, v61
	v_mul_f32_e32 v62, 0x43000000, v62
	v_mul_f32_e32 v63, 0x43000000, v63
	ds_write_b128 v4, v[60:63] offset:6144
	v_mul_f32_e32 v64, 0x43000000, v64
	v_mul_f32_e32 v65, 0x43000000, v65
	v_mul_f32_e32 v66, 0x43000000, v66
	v_mul_f32_e32 v67, 0x43000000, v67
	ds_write_b128 v4, v[64:67] offset:7168
	s_waitcnt lgkmcnt(0)
	s_barrier
; #define GAS __attribute__((address_space(1)))
; #define LAS __attribute__((address_space(3)))
; #define LDS_WAIT() asm volatile("s_waitcnt lgkmcnt(0)" ::: "memory")
;     const int pr = item >> 1, kb = 2 * (pr / nblk) + (item & 1), nb = pr % nblk, k0 = 64 * kb, n0 = 32 * nb;
;     const int nr = n0 + (lane & 31); const int sc = MAP == 1 ? src_col_in(nr) : nr;
;     float v[32];
; #pragma unroll
;     for (int i = 0; i < 32; ++i) v[i] = sc >= 0 ? W[(size_t)(k0 + 2 * i + (lane >> 5)) * Nsrc + sc] : 0.f;
; #pragma unroll
;     for (int i = 0; i < 32; ++i) { const int k = k0 + 2 * i + (lane >> 5); float x = v[i] * wscale; if (KS) x *= (k < ksplit ? ksA[k] : ksB[k - ksplit]); scr[(2 * i + (lane >> 5)) * 33 + (lane & 31)] = x; }
;     LDS_WAIT(); asm volatile("" ::: "memory");
;     const int c = lane & 7;
; #pragma unroll
;     for (int j = 0; j < 4; ++j) { const int n = (lane >> 3) + 8 * j; const LAS float* s = scr + (8 * c) * 33 + n;
;         const unsigned long long o = (unsigned long long)pg8::pk4_fp8(s[0 * 33], s[1 * 33], s[2 * 33], s[3 * 33]) | ((unsigned long long)pg8::pk4_fp8(s[4 * 33], s[5 * 33], s[6 * 33], s[7 * 33]) << 32);
;         *(GAS unsigned long long*)(WT + (size_t)(n0 + n) * K + k0 + 8 * c) = o; }
;     LDS_WAIT(); asm volatile("" ::: "memory");
; }
; __global__ void __launch_bounds__(NWAVES * 64, 2) hybrid_fwd(Args args) {
;     ...
;             p0_transpose_item_f8<false>(args.in[16] + (size_t)l * FF * DM, FF, DM, DM / 32, (unsigned char*)(ws + WS_WDN + l * SZ_WDN), 128.f, args.in[16], args.in[16], 0, scr, r, lane);
	s_add_i32 s17, s16, 3456
	s_min_u32 s17, s17, 0xfff
	s_lshr_b32 s18, s17, 5
	s_add_i32 s18, s18, 0
	s_and_b32 s19, s17, 31
	s_lshl_b32 s18, s18, 21
	s_lshl_b32 s19, s19, 9
	s_add_u32 s18, s18, s19
	s_add_u32 s12, s2, s18
	s_addc_u32 s13, s3, 0
	global_load_dwordx4 v[36:39], v10, s[12:13]
	s_add_u32 s12, s12, 0x8000
	s_addc_u32 s13, s13, 0
	global_load_dwordx4 v[40:43], v10, s[12:13]
	s_add_u32 s12, s12, 0x8000
	s_addc_u32 s13, s13, 0
	global_load_dwordx4 v[44:47], v10, s[12:13]
	s_add_u32 s12, s12, 0x8000
	s_addc_u32 s13, s13, 0
	global_load_dwordx4 v[48:51], v10, s[12:13]
	s_add_u32 s12, s12, 0x8000
	s_addc_u32 s13, s13, 0
	global_load_dwordx4 v[52:55], v10, s[12:13]
	s_add_u32 s12, s12, 0x8000
	s_addc_u32 s13, s13, 0
	global_load_dwordx4 v[56:59], v10, s[12:13]
	s_add_u32 s12, s12, 0x8000
	s_addc_u32 s13, s13, 0
	global_load_dwordx4 v[60:63], v10, s[12:13]
	s_add_u32 s12, s12, 0x8000
	s_addc_u32 s13, s13, 0
	global_load_dwordx4 v[64:67], v10, s[12:13]
	s_add_i32 s17, s16, 3072
	s_min_u32 s17, s17, 0xfff
	s_lshr_b32 s18, s17, 5
	s_add_i32 s18, s18, 0
	s_and_b32 s19, s17, 31
	s_lshl_b32 s19, s19, 21
	s_lshl_b32 s18, s18, 7
	s_add_u32 s18, s18, s19
	s_add_u32 s14, s4, s18
	s_addc_u32 s15, s5, 0
	ds_read_b32 v170, v6
	ds_read_b32 v171, v6 offset:512
	ds_read_b32 v172, v6 offset:1024
	ds_read_b32 v173, v6 offset:1536
	ds_read_b32 v174, v6 offset:2048
	ds_read_b32 v175, v6 offset:2560
	ds_read_b32 v176, v6 offset:3072
	ds_read_b32 v177, v6 offset:3584
	ds_read_b32 v196, v6 offset:4096
	ds_read_b32 v197, v6 offset:4608
	ds_read_b32 v198, v6 offset:5120
	ds_read_b32 v199, v6 offset:5632
	ds_read_b32 v200, v6 offset:6144
	ds_read_b32 v201, v6 offset:6656
	ds_read_b32 v202, v6 offset:7168
	ds_read_b32 v203, v6 offset:7680
	s_waitcnt lgkmcnt(0)
	v_max_f32_e32 v170, v170, v170
	v_max_f32_e32 v171, v171, v171
	v_max_f32_e32 v172, v172, v172
	v_max_f32_e32 v173, v173, v173
	v_max_f32_e32 v174, v174, v174
	v_max_f32_e32 v175, v175, v175
	v_max_f32_e32 v176, v176, v176
	v_max_f32_e32 v177, v177, v177
	v_max_f32_e32 v196, v196, v196
	v_max_f32_e32 v197, v197, v197
	v_max_f32_e32 v198, v198, v198
	v_max_f32_e32 v199, v199, v199
	v_max_f32_e32 v200, v200, v200
	v_max_f32_e32 v201, v201, v201
	v_max_f32_e32 v202, v202, v202
	v_max_f32_e32 v203, v203, v203
	v_med3_f32 v170, v170, s20, v13
	v_med3_f32 v171, v171, s20, v13
	v_med3_f32 v172, v172, s20, v13
	v_med3_f32 v173, v173, s20, v13
	v_med3_f32 v174, v174, s20, v13
	v_med3_f32 v175, v175, s20, v13
	v_med3_f32 v176, v176, s20, v13
	v_med3_f32 v177, v177, s20, v13
	v_med3_f32 v196, v196, s20, v13
	v_med3_f32 v197, v197, s20, v13
	v_med3_f32 v198, v198, s20, v13
	v_med3_f32 v199, v199, s20, v13
	v_med3_f32 v200, v200, s20, v13
	v_med3_f32 v201, v201, s20, v13
	v_med3_f32 v202, v202, s20, v13
	v_med3_f32 v203, v203, s20, v13
	v_mov_b32_e32 v208, 0
	v_mov_b32_e32 v209, 0
	v_mov_b32_e32 v210, 0
	v_mov_b32_e32 v211, 0
	v_cvt_pk_fp8_f32 v208, v170, v171
	v_cvt_pk_fp8_f32 v209, v174, v175
	v_cvt_pk_fp8_f32 v210, v196, v197
	v_cvt_pk_fp8_f32 v211, v200, v201
	v_cvt_pk_fp8_f32 v208, v172, v173 op_sel:[0,0,1]
	v_cvt_pk_fp8_f32 v209, v176, v177 op_sel:[0,0,1]
	v_cvt_pk_fp8_f32 v210, v198, v199 op_sel:[0,0,1]
	v_cvt_pk_fp8_f32 v211, v202, v203 op_sel:[0,0,1]
	s_nop 0
	global_store_dwordx4 v11, v[208:211], s[14:15]
	ds_read_b32 v170, v8
	ds_read_b32 v171, v8 offset:512
	ds_read_b32 v172, v8 offset:1024
	ds_read_b32 v173, v8 offset:1536
	ds_read_b32 v174, v8 offset:2048
	ds_read_b32 v175, v8 offset:2560
	ds_read_b32 v176, v8 offset:3072
	ds_read_b32 v177, v8 offset:3584
	ds_read_b32 v196, v8 offset:4096
	ds_read_b32 v197, v8 offset:4608
	ds_read_b32 v198, v8 offset:5120
	ds_read_b32 v199, v8 offset:5632
	ds_read_b32 v200, v8 offset:6144
	ds_read_b32 v201, v8 offset:6656
	ds_read_b32 v202, v8 offset:7168
	ds_read_b32 v203, v8 offset:7680
	s_waitcnt lgkmcnt(0)
	v_max_f32_e32 v170, v170, v170
	v_max_f32_e32 v171, v171, v171
	v_max_f32_e32 v172, v172, v172
	v_max_f32_e32 v173, v173, v173
	v_max_f32_e32 v174, v174, v174
	v_max_f32_e32 v175, v175, v175
	v_max_f32_e32 v176, v176, v176
	v_max_f32_e32 v177, v177, v177
	v_max_f32_e32 v196, v196, v196
	v_max_f32_e32 v197, v197, v197
	v_max_f32_e32 v198, v198, v198
	v_max_f32_e32 v199, v199, v199
	v_max_f32_e32 v200, v200, v200
	v_max_f32_e32 v201, v201, v201
	v_max_f32_e32 v202, v202, v202
	v_max_f32_e32 v203, v203, v203
	v_med3_f32 v170, v170, s20, v13
	v_med3_f32 v171, v171, s20, v13
	v_med3_f32 v172, v172, s20, v13
	v_med3_f32 v173, v173, s20, v13
	v_med3_f32 v174, v174, s20, v13
	v_med3_f32 v175, v175, s20, v13
	v_med3_f32 v176, v176, s20, v13
	v_med3_f32 v177, v177, s20, v13
	v_med3_f32 v196, v196, s20, v13
	v_med3_f32 v197, v197, s20, v13
	v_med3_f32 v198, v198, s20, v13
	v_med3_f32 v199, v199, s20, v13
	v_med3_f32 v200, v200, s20, v13
	v_med3_f32 v201, v201, s20, v13
	v_med3_f32 v202, v202, s20, v13
	v_med3_f32 v203, v203, s20, v13
	v_mov_b32_e32 v208, 0
	v_mov_b32_e32 v209, 0
	v_mov_b32_e32 v210, 0
	v_mov_b32_e32 v211, 0
	v_cvt_pk_fp8_f32 v208, v170, v171
	v_cvt_pk_fp8_f32 v209, v174, v175
	v_cvt_pk_fp8_f32 v210, v196, v197
	v_cvt_pk_fp8_f32 v211, v200, v201
	v_cvt_pk_fp8_f32 v208, v172, v173 op_sel:[0,0,1]
	v_cvt_pk_fp8_f32 v209, v176, v177 op_sel:[0,0,1]
	v_cvt_pk_fp8_f32 v210, v198, v199 op_sel:[0,0,1]
	v_cvt_pk_fp8_f32 v211, v202, v203 op_sel:[0,0,1]
	s_nop 0
	global_store_dwordx4 v12, v[208:211], s[14:15]
	s_waitcnt vmcnt(32)
	v_mul_f32_e32 v68, 0x43000000, v68
	v_mul_f32_e32 v69, 0x43000000, v69
	v_mul_f32_e32 v70, 0x43000000, v70
	v_mul_f32_e32 v71, 0x43000000, v71
	ds_write_b128 v5, v[68:71]
	v_mul_f32_e32 v72, 0x43000000, v72
	v_mul_f32_e32 v73, 0x43000000, v73
	v_mul_f32_e32 v74, 0x43000000, v74
	v_mul_f32_e32 v75, 0x43000000, v75
	ds_write_b128 v5, v[72:75] offset:1024
	v_mul_f32_e32 v76, 0x43000000, v76
	v_mul_f32_e32 v77, 0x43000000, v77
	v_mul_f32_e32 v78, 0x43000000, v78
	v_mul_f32_e32 v79, 0x43000000, v79
	ds_write_b128 v5, v[76:79] offset:2048
	v_mul_f32_e32 v80, 0x43000000, v80
	v_mul_f32_e32 v81, 0x43000000, v81
	v_mul_f32_e32 v82, 0x43000000, v82
	v_mul_f32_e32 v83, 0x43000000, v83
	ds_write_b128 v5, v[80:83] offset:3072
	v_mul_f32_e32 v84, 0x43000000, v84
	v_mul_f32_e32 v85, 0x43000000, v85
	v_mul_f32_e32 v86, 0x43000000, v86
	v_mul_f32_e32 v87, 0x43000000, v87
	ds_write_b128 v5, v[84:87] offset:4096
	v_mul_f32_e32 v88, 0x43000000, v88
	v_mul_f32_e32 v89, 0x43000000, v89
	v_mul_f32_e32 v90, 0x43000000, v90
	v_mul_f32_e32 v91, 0x43000000, v91
	ds_write_b128 v5, v[88:91] offset:5120
	v_mul_f32_e32 v92, 0x43000000, v92
	v_mul_f32_e32 v93, 0x43000000, v93
	v_mul_f32_e32 v94, 0x43000000, v94
	v_mul_f32_e32 v95, 0x43000000, v95
	ds_write_b128 v5, v[92:95] offset:6144
	v_mul_f32_e32 v96, 0x43000000, v96
	v_mul_f32_e32 v97, 0x43000000, v97
	v_mul_f32_e32 v98, 0x43000000, v98
	v_mul_f32_e32 v99, 0x43000000, v99
	ds_write_b128 v5, v[96:99] offset:7168
	s_waitcnt lgkmcnt(0)
	s_barrier
; #define GAS __attribute__((address_space(1)))
; #define LAS __attribute__((address_space(3)))
; #define LDS_WAIT() asm volatile("s_waitcnt lgkmcnt(0)" ::: "memory")
;     const int pr = item >> 1, kb = 2 * (pr / nblk) + (item & 1), nb = pr % nblk, k0 = 64 * kb, n0 = 32 * nb;
;     const int nr = n0 + (lane & 31); const int sc = MAP == 1 ? src_col_in(nr) : nr;
;     float v[32];
; #pragma unroll
;     for (int i = 0; i < 32; ++i) v[i] = sc >= 0 ? W[(size_t)(k0 + 2 * i + (lane >> 5)) * Nsrc + sc] : 0.f;
; #pragma unroll
;     for (int i = 0; i < 32; ++i) { const int k = k0 + 2 * i + (lane >> 5); float x = v[i] * wscale; if (KS) x *= (k < ksplit ? ksA[k] : ksB[k - ksplit]); scr[(2 * i + (lane >> 5)) * 33 + (lane & 31)] = x; }
;     LDS_WAIT(); asm volatile("" ::: "memory");
;     const int c = lane & 7;
; #pragma unroll
;     for (int j = 0; j < 4; ++j) { const int n = (lane >> 3) + 8 * j; const LAS float* s = scr + (8 * c) * 33 + n;
;         const unsigned long long o = (unsigned long long)pg8::pk4_fp8(s[0 * 33], s[1 * 33], s[2 * 33], s[3 * 33]) | ((unsigned long long)pg8::pk4_fp8(s[4 * 33], s[5 * 33], s[6 * 33], s[7 * 33]) << 32);
;         *(GAS unsigned long long*)(WT + (size_t)(n0 + n) * K + k0 + 8 * c) = o; }
;     LDS_WAIT(); asm volatile("" ::: "memory");
; }
; __global__ void __launch_bounds__(NWAVES * 64, 2) hybrid_fwd(Args args) {
;     ...
;             p0_transpose_item_f8<false>(args.in[16] + (size_t)l * FF * DM, FF, DM, DM / 32, (unsigned char*)(ws + WS_WDN + l * SZ_WDN), 128.f, args.in[16], args.in[16], 0, scr, r, lane);
	s_add_i32 s17, s16, 3552
	s_min_u32 s17, s17, 0xfff
	s_lshr_b32 s18, s17, 5
	s_add_i32 s18, s18, 0
	s_and_b32 s19, s17, 31
	s_lshl_b32 s18, s18, 21
	s_lshl_b32 s19, s19, 9
	s_add_u32 s18, s18, s19
	s_add_u32 s12, s2, s18
	s_addc_u32 s13, s3, 0
	global_load_dwordx4 v[68:71], v10, s[12:13]
	s_add_u32 s12, s12, 0x8000
	s_addc_u32 s13, s13, 0
	global_load_dwordx4 v[72:75], v10, s[12:13]
	s_add_u32 s12, s12, 0x8000
	s_addc_u32 s13, s13, 0
	global_load_dwordx4 v[76:79], v10, s[12:13]
	s_add_u32 s12, s12, 0x8000
	s_addc_u32 s13, s13, 0
	global_load_dwordx4 v[80:83], v10, s[12:13]
	s_add_u32 s12, s12, 0x8000
	s_addc_u32 s13, s13, 0
	global_load_dwordx4 v[84:87], v10, s[12:13]
	s_add_u32 s12, s12, 0x8000
	s_addc_u32 s13, s13, 0
	global_load_dwordx4 v[88:91], v10, s[12:13]
	s_add_u32 s12, s12, 0x8000
	s_addc_u32 s13, s13, 0
	global_load_dwordx4 v[92:95], v10, s[12:13]
	s_add_u32 s12, s12, 0x8000
	s_addc_u32 s13, s13, 0
	global_load_dwordx4 v[96:99], v10, s[12:13]
	s_add_i32 s17, s16, 3168
	s_min_u32 s17, s17, 0xfff
	s_lshr_b32 s18, s17, 5
	s_add_i32 s18, s18, 0
	s_and_b32 s19, s17, 31
	s_lshl_b32 s19, s19, 21
	s_lshl_b32 s18, s18, 7
	s_add_u32 s18, s18, s19
	s_add_u32 s14, s4, s18
	s_addc_u32 s15, s5, 0
	ds_read_b32 v170, v7
	ds_read_b32 v171, v7 offset:512
	ds_read_b32 v172, v7 offset:1024
	ds_read_b32 v173, v7 offset:1536
	ds_read_b32 v174, v7 offset:2048
	ds_read_b32 v175, v7 offset:2560
	ds_read_b32 v176, v7 offset:3072
	ds_read_b32 v177, v7 offset:3584
	ds_read_b32 v196, v7 offset:4096
	ds_read_b32 v197, v7 offset:4608
	ds_read_b32 v198, v7 offset:5120
	ds_read_b32 v199, v7 offset:5632
	ds_read_b32 v200, v7 offset:6144
	ds_read_b32 v201, v7 offset:6656
	ds_read_b32 v202, v7 offset:7168
	ds_read_b32 v203, v7 offset:7680
	s_waitcnt lgkmcnt(0)
	v_max_f32_e32 v170, v170, v170
	v_max_f32_e32 v171, v171, v171
	v_max_f32_e32 v172, v172, v172
	v_max_f32_e32 v173, v173, v173
	v_max_f32_e32 v174, v174, v174
	v_max_f32_e32 v175, v175, v175
	v_max_f32_e32 v176, v176, v176
	v_max_f32_e32 v177, v177, v177
	v_max_f32_e32 v196, v196, v196
	v_max_f32_e32 v197, v197, v197
	v_max_f32_e32 v198, v198, v198
	v_max_f32_e32 v199, v199, v199
	v_max_f32_e32 v200, v200, v200
	v_max_f32_e32 v201, v201, v201
	v_max_f32_e32 v202, v202, v202
	v_max_f32_e32 v203, v203, v203
	v_med3_f32 v170, v170, s20, v13
	v_med3_f32 v171, v171, s20, v13
	v_med3_f32 v172, v172, s20, v13
	v_med3_f32 v173, v173, s20, v13
	v_med3_f32 v174, v174, s20, v13
	v_med3_f32 v175, v175, s20, v13
	v_med3_f32 v176, v176, s20, v13
	v_med3_f32 v177, v177, s20, v13
	v_med3_f32 v196, v196, s20, v13
	v_med3_f32 v197, v197, s20, v13
	v_med3_f32 v198, v198, s20, v13
	v_med3_f32 v199, v199, s20, v13
	v_med3_f32 v200, v200, s20, v13
	v_med3_f32 v201, v201, s20, v13
	v_med3_f32 v202, v202, s20, v13
	v_med3_f32 v203, v203, s20, v13
	v_mov_b32_e32 v208, 0
	v_mov_b32_e32 v209, 0
	v_mov_b32_e32 v210, 0
	v_mov_b32_e32 v211, 0
	v_cvt_pk_fp8_f32 v208, v170, v171
	v_cvt_pk_fp8_f32 v209, v174, v175
	v_cvt_pk_fp8_f32 v210, v196, v197
	v_cvt_pk_fp8_f32 v211, v200, v201
	v_cvt_pk_fp8_f32 v208, v172, v173 op_sel:[0,0,1]
	v_cvt_pk_fp8_f32 v209, v176, v177 op_sel:[0,0,1]
	v_cvt_pk_fp8_f32 v210, v198, v199 op_sel:[0,0,1]
	v_cvt_pk_fp8_f32 v211, v202, v203 op_sel:[0,0,1]
	s_nop 0
	global_store_dwordx4 v11, v[208:211], s[14:15]
	ds_read_b32 v170, v9
	ds_read_b32 v171, v9 offset:512
	ds_read_b32 v172, v9 offset:1024
	ds_read_b32 v173, v9 offset:1536
	ds_read_b32 v174, v9 offset:2048
	ds_read_b32 v175, v9 offset:2560
	ds_read_b32 v176, v9 offset:3072
	ds_read_b32 v177, v9 offset:3584
	ds_read_b32 v196, v9 offset:4096
	ds_read_b32 v197, v9 offset:4608
	ds_read_b32 v198, v9 offset:5120
	ds_read_b32 v199, v9 offset:5632
	ds_read_b32 v200, v9 offset:6144
	ds_read_b32 v201, v9 offset:6656
	ds_read_b32 v202, v9 offset:7168
	ds_read_b32 v203, v9 offset:7680
	s_waitcnt lgkmcnt(0)
	v_max_f32_e32 v170, v170, v170
	v_max_f32_e32 v171, v171, v171
	v_max_f32_e32 v172, v172, v172
	v_max_f32_e32 v173, v173, v173
	v_max_f32_e32 v174, v174, v174
	v_max_f32_e32 v175, v175, v175
	v_max_f32_e32 v176, v176, v176
	v_max_f32_e32 v177, v177, v177
	v_max_f32_e32 v196, v196, v196
	v_max_f32_e32 v197, v197, v197
	v_max_f32_e32 v198, v198, v198
	v_max_f32_e32 v199, v199, v199
	v_max_f32_e32 v200, v200, v200
	v_max_f32_e32 v201, v201, v201
	v_max_f32_e32 v202, v202, v202
	v_max_f32_e32 v203, v203, v203
	v_med3_f32 v170, v170, s20, v13
	v_med3_f32 v171, v171, s20, v13
	v_med3_f32 v172, v172, s20, v13
	v_med3_f32 v173, v173, s20, v13
	v_med3_f32 v174, v174, s20, v13
	v_med3_f32 v175, v175, s20, v13
	v_med3_f32 v176, v176, s20, v13
	v_med3_f32 v177, v177, s20, v13
	v_med3_f32 v196, v196, s20, v13
	v_med3_f32 v197, v197, s20, v13
	v_med3_f32 v198, v198, s20, v13
	v_med3_f32 v199, v199, s20, v13
	v_med3_f32 v200, v200, s20, v13
	v_med3_f32 v201, v201, s20, v13
	v_med3_f32 v202, v202, s20, v13
	v_med3_f32 v203, v203, s20, v13
	v_mov_b32_e32 v208, 0
	v_mov_b32_e32 v209, 0
	v_mov_b32_e32 v210, 0
	v_mov_b32_e32 v211, 0
	v_cvt_pk_fp8_f32 v208, v170, v171
	v_cvt_pk_fp8_f32 v209, v174, v175
	v_cvt_pk_fp8_f32 v210, v196, v197
	v_cvt_pk_fp8_f32 v211, v200, v201
	v_cvt_pk_fp8_f32 v208, v172, v173 op_sel:[0,0,1]
	v_cvt_pk_fp8_f32 v209, v176, v177 op_sel:[0,0,1]
	v_cvt_pk_fp8_f32 v210, v198, v199 op_sel:[0,0,1]
	v_cvt_pk_fp8_f32 v211, v202, v203 op_sel:[0,0,1]
	s_nop 0
	global_store_dwordx4 v12, v[208:211], s[14:15]
	s_waitcnt vmcnt(32)
	v_mul_f32_e32 v100, 0x43000000, v100
	v_mul_f32_e32 v101, 0x43000000, v101
	v_mul_f32_e32 v102, 0x43000000, v102
	v_mul_f32_e32 v103, 0x43000000, v103
	ds_write_b128 v4, v[100:103]
	v_mul_f32_e32 v104, 0x43000000, v104
	v_mul_f32_e32 v105, 0x43000000, v105
	v_mul_f32_e32 v106, 0x43000000, v106
	v_mul_f32_e32 v107, 0x43000000, v107
	ds_write_b128 v4, v[104:107] offset:1024
	v_mul_f32_e32 v108, 0x43000000, v108
	v_mul_f32_e32 v109, 0x43000000, v109
	v_mul_f32_e32 v110, 0x43000000, v110
	v_mul_f32_e32 v111, 0x43000000, v111
	ds_write_b128 v4, v[108:111] offset:2048
	v_mul_f32_e32 v112, 0x43000000, v112
	v_mul_f32_e32 v113, 0x43000000, v113
	v_mul_f32_e32 v114, 0x43000000, v114
	v_mul_f32_e32 v115, 0x43000000, v115
	ds_write_b128 v4, v[112:115] offset:3072
	v_mul_f32_e32 v116, 0x43000000, v116
	v_mul_f32_e32 v117, 0x43000000, v117
	v_mul_f32_e32 v118, 0x43000000, v118
	v_mul_f32_e32 v119, 0x43000000, v119
	ds_write_b128 v4, v[116:119] offset:4096
	v_mul_f32_e32 v120, 0x43000000, v120
	v_mul_f32_e32 v121, 0x43000000, v121
	v_mul_f32_e32 v122, 0x43000000, v122
	v_mul_f32_e32 v123, 0x43000000, v123
	ds_write_b128 v4, v[120:123] offset:5120
	v_mul_f32_e32 v124, 0x43000000, v124
	v_mul_f32_e32 v125, 0x43000000, v125
	v_mul_f32_e32 v126, 0x43000000, v126
	v_mul_f32_e32 v127, 0x43000000, v127
	ds_write_b128 v4, v[124:127] offset:6144
	v_mul_f32_e32 v128, 0x43000000, v128
	v_mul_f32_e32 v129, 0x43000000, v129
	v_mul_f32_e32 v130, 0x43000000, v130
	v_mul_f32_e32 v131, 0x43000000, v131
	ds_write_b128 v4, v[128:131] offset:7168
	s_waitcnt lgkmcnt(0)
	s_barrier
; #define GAS __attribute__((address_space(1)))
; #define LAS __attribute__((address_space(3)))
; #define LDS_WAIT() asm volatile("s_waitcnt lgkmcnt(0)" ::: "memory")
;     const int pr = item >> 1, kb = 2 * (pr / nblk) + (item & 1), nb = pr % nblk, k0 = 64 * kb, n0 = 32 * nb;
;     const int nr = n0 + (lane & 31); const int sc = MAP == 1 ? src_col_in(nr) : nr;
;     float v[32];
; #pragma unroll
;     for (int i = 0; i < 32; ++i) v[i] = sc >= 0 ? W[(size_t)(k0 + 2 * i + (lane >> 5)) * Nsrc + sc] : 0.f;
; #pragma unroll
;     for (int i = 0; i < 32; ++i) { const int k = k0 + 2 * i + (lane >> 5); float x = v[i] * wscale; if (KS) x *= (k < ksplit ? ksA[k] : ksB[k - ksplit]); scr[(2 * i + (lane >> 5)) * 33 + (lane & 31)] = x; }
;     LDS_WAIT(); asm volatile("" ::: "memory");
;     const int c = lane & 7;
; #pragma unroll
;     for (int j = 0; j < 4; ++j) { const int n = (lane >> 3) + 8 * j; const LAS float* s = scr + (8 * c) * 33 + n;
;         const unsigned long long o = (unsigned long long)pg8::pk4_fp8(s[0 * 33], s[1 * 33], s[2 * 33], s[3 * 33]) | ((unsigned long long)pg8::pk4_fp8(s[4 * 33], s[5 * 33], s[6 * 33], s[7 * 33]) << 32);
;         *(GAS unsigned long long*)(WT + (size_t)(n0 + n) * K + k0 + 8 * c) = o; }
;     LDS_WAIT(); asm volatile("" ::: "memory");
; }
; __global__ void __launch_bounds__(NWAVES * 64, 2) hybrid_fwd(Args args) {
;     ...
;             p0_transpose_item_f8<false>(args.in[16] + (size_t)l * FF * DM, FF, DM, DM / 32, (unsigned char*)(ws + WS_WDN + l * SZ_WDN), 128.f, args.in[16], args.in[16], 0, scr, r, lane);
	s_add_i32 s17, s16, 3648
	s_min_u32 s17, s17, 0xfff
	s_lshr_b32 s18, s17, 5
	s_add_i32 s18, s18, 0
	s_and_b32 s19, s17, 31
	s_lshl_b32 s18, s18, 21
	s_lshl_b32 s19, s19, 9
	s_add_u32 s18, s18, s19
	s_add_u32 s12, s2, s18
	s_addc_u32 s13, s3, 0
	global_load_dwordx4 v[100:103], v10, s[12:13]
	s_add_u32 s12, s12, 0x8000
	s_addc_u32 s13, s13, 0
	global_load_dwordx4 v[104:107], v10, s[12:13]
	s_add_u32 s12, s12, 0x8000
	s_addc_u32 s13, s13, 0
	global_load_dwordx4 v[108:111], v10, s[12:13]
	s_add_u32 s12, s12, 0x8000
	s_addc_u32 s13, s13, 0
	global_load_dwordx4 v[112:115], v10, s[12:13]
	s_add_u32 s12, s12, 0x8000
	s_addc_u32 s13, s13, 0
	global_load_dwordx4 v[116:119], v10, s[12:13]
	s_add_u32 s12, s12, 0x8000
	s_addc_u32 s13, s13, 0
	global_load_dwordx4 v[120:123], v10, s[12:13]
	s_add_u32 s12, s12, 0x8000
	s_addc_u32 s13, s13, 0
	global_load_dwordx4 v[124:127], v10, s[12:13]
	s_add_u32 s12, s12, 0x8000
	s_addc_u32 s13, s13, 0
	global_load_dwordx4 v[128:131], v10, s[12:13]
	s_add_i32 s17, s16, 3264
	s_min_u32 s17, s17, 0xfff
	s_lshr_b32 s18, s17, 5
	s_add_i32 s18, s18, 0
	s_and_b32 s19, s17, 31
	s_lshl_b32 s19, s19, 21
	s_lshl_b32 s18, s18, 7
	s_add_u32 s18, s18, s19
	s_add_u32 s14, s4, s18
	s_addc_u32 s15, s5, 0
	ds_read_b32 v170, v6
	ds_read_b32 v171, v6 offset:512
	ds_read_b32 v172, v6 offset:1024
	ds_read_b32 v173, v6 offset:1536
	ds_read_b32 v174, v6 offset:2048
	ds_read_b32 v175, v6 offset:2560
	ds_read_b32 v176, v6 offset:3072
	ds_read_b32 v177, v6 offset:3584
	ds_read_b32 v196, v6 offset:4096
	ds_read_b32 v197, v6 offset:4608
	ds_read_b32 v198, v6 offset:5120
	ds_read_b32 v199, v6 offset:5632
	ds_read_b32 v200, v6 offset:6144
	ds_read_b32 v201, v6 offset:6656
	ds_read_b32 v202, v6 offset:7168
	ds_read_b32 v203, v6 offset:7680
	s_waitcnt lgkmcnt(0)
	v_max_f32_e32 v170, v170, v170
	v_max_f32_e32 v171, v171, v171
	v_max_f32_e32 v172, v172, v172
	v_max_f32_e32 v173, v173, v173
	v_max_f32_e32 v174, v174, v174
	v_max_f32_e32 v175, v175, v175
	v_max_f32_e32 v176, v176, v176
	v_max_f32_e32 v177, v177, v177
	v_max_f32_e32 v196, v196, v196
	v_max_f32_e32 v197, v197, v197
	v_max_f32_e32 v198, v198, v198
	v_max_f32_e32 v199, v199, v199
	v_max_f32_e32 v200, v200, v200
	v_max_f32_e32 v201, v201, v201
	v_max_f32_e32 v202, v202, v202
	v_max_f32_e32 v203, v203, v203
	v_med3_f32 v170, v170, s20, v13
	v_med3_f32 v171, v171, s20, v13
	v_med3_f32 v172, v172, s20, v13
	v_med3_f32 v173, v173, s20, v13
	v_med3_f32 v174, v174, s20, v13
	v_med3_f32 v175, v175, s20, v13
	v_med3_f32 v176, v176, s20, v13
	v_med3_f32 v177, v177, s20, v13
	v_med3_f32 v196, v196, s20, v13
	v_med3_f32 v197, v197, s20, v13
	v_med3_f32 v198, v198, s20, v13
	v_med3_f32 v199, v199, s20, v13
	v_med3_f32 v200, v200, s20, v13
	v_med3_f32 v201, v201, s20, v13
	v_med3_f32 v202, v202, s20, v13
	v_med3_f32 v203, v203, s20, v13
	v_mov_b32_e32 v208, 0
	v_mov_b32_e32 v209, 0
	v_mov_b32_e32 v210, 0
	v_mov_b32_e32 v211, 0
	v_cvt_pk_fp8_f32 v208, v170, v171
	v_cvt_pk_fp8_f32 v209, v174, v175
	v_cvt_pk_fp8_f32 v210, v196, v197
	v_cvt_pk_fp8_f32 v211, v200, v201
	v_cvt_pk_fp8_f32 v208, v172, v173 op_sel:[0,0,1]
	v_cvt_pk_fp8_f32 v209, v176, v177 op_sel:[0,0,1]
	v_cvt_pk_fp8_f32 v210, v198, v199 op_sel:[0,0,1]
	v_cvt_pk_fp8_f32 v211, v202, v203 op_sel:[0,0,1]
	s_nop 0
	global_store_dwordx4 v11, v[208:211], s[14:15]
	ds_read_b32 v170, v8
	ds_read_b32 v171, v8 offset:512
	ds_read_b32 v172, v8 offset:1024
	ds_read_b32 v173, v8 offset:1536
	ds_read_b32 v174, v8 offset:2048
	ds_read_b32 v175, v8 offset:2560
	ds_read_b32 v176, v8 offset:3072
	ds_read_b32 v177, v8 offset:3584
	ds_read_b32 v196, v8 offset:4096
	ds_read_b32 v197, v8 offset:4608
	ds_read_b32 v198, v8 offset:5120
	ds_read_b32 v199, v8 offset:5632
	ds_read_b32 v200, v8 offset:6144
	ds_read_b32 v201, v8 offset:6656
	ds_read_b32 v202, v8 offset:7168
	ds_read_b32 v203, v8 offset:7680
	s_waitcnt lgkmcnt(0)
	v_max_f32_e32 v170, v170, v170
	v_max_f32_e32 v171, v171, v171
	v_max_f32_e32 v172, v172, v172
	v_max_f32_e32 v173, v173, v173
	v_max_f32_e32 v174, v174, v174
	v_max_f32_e32 v175, v175, v175
	v_max_f32_e32 v176, v176, v176
	v_max_f32_e32 v177, v177, v177
	v_max_f32_e32 v196, v196, v196
	v_max_f32_e32 v197, v197, v197
	v_max_f32_e32 v198, v198, v198
	v_max_f32_e32 v199, v199, v199
	v_max_f32_e32 v200, v200, v200
	v_max_f32_e32 v201, v201, v201
	v_max_f32_e32 v202, v202, v202
	v_max_f32_e32 v203, v203, v203
	v_med3_f32 v170, v170, s20, v13
	v_med3_f32 v171, v171, s20, v13
	v_med3_f32 v172, v172, s20, v13
	v_med3_f32 v173, v173, s20, v13
	v_med3_f32 v174, v174, s20, v13
	v_med3_f32 v175, v175, s20, v13
	v_med3_f32 v176, v176, s20, v13
	v_med3_f32 v177, v177, s20, v13
	v_med3_f32 v196, v196, s20, v13
	v_med3_f32 v197, v197, s20, v13
	v_med3_f32 v198, v198, s20, v13
	v_med3_f32 v199, v199, s20, v13
	v_med3_f32 v200, v200, s20, v13
	v_med3_f32 v201, v201, s20, v13
	v_med3_f32 v202, v202, s20, v13
	v_med3_f32 v203, v203, s20, v13
	v_mov_b32_e32 v208, 0
	v_mov_b32_e32 v209, 0
	v_mov_b32_e32 v210, 0
	v_mov_b32_e32 v211, 0
	v_cvt_pk_fp8_f32 v208, v170, v171
	v_cvt_pk_fp8_f32 v209, v174, v175
	v_cvt_pk_fp8_f32 v210, v196, v197
	v_cvt_pk_fp8_f32 v211, v200, v201
	v_cvt_pk_fp8_f32 v208, v172, v173 op_sel:[0,0,1]
	v_cvt_pk_fp8_f32 v209, v176, v177 op_sel:[0,0,1]
	v_cvt_pk_fp8_f32 v210, v198, v199 op_sel:[0,0,1]
	v_cvt_pk_fp8_f32 v211, v202, v203 op_sel:[0,0,1]
	s_nop 0
	global_store_dwordx4 v12, v[208:211], s[14:15]
	s_waitcnt vmcnt(32)
	v_mul_f32_e32 v132, 0x43000000, v132
	v_mul_f32_e32 v133, 0x43000000, v133
	v_mul_f32_e32 v134, 0x43000000, v134
	v_mul_f32_e32 v135, 0x43000000, v135
	ds_write_b128 v5, v[132:135]
	v_mul_f32_e32 v136, 0x43000000, v136
	v_mul_f32_e32 v137, 0x43000000, v137
	v_mul_f32_e32 v138, 0x43000000, v138
	v_mul_f32_e32 v139, 0x43000000, v139
	ds_write_b128 v5, v[136:139] offset:1024
	v_mul_f32_e32 v140, 0x43000000, v140
	v_mul_f32_e32 v141, 0x43000000, v141
	v_mul_f32_e32 v142, 0x43000000, v142
	v_mul_f32_e32 v143, 0x43000000, v143
	ds_write_b128 v5, v[140:143] offset:2048
	v_mul_f32_e32 v144, 0x43000000, v144
	v_mul_f32_e32 v145, 0x43000000, v145
	v_mul_f32_e32 v146, 0x43000000, v146
	v_mul_f32_e32 v147, 0x43000000, v147
	ds_write_b128 v5, v[144:147] offset:3072
	v_mul_f32_e32 v148, 0x43000000, v148
	v_mul_f32_e32 v149, 0x43000000, v149
	v_mul_f32_e32 v150, 0x43000000, v150
	v_mul_f32_e32 v151, 0x43000000, v151
	ds_write_b128 v5, v[148:151] offset:4096
	v_mul_f32_e32 v152, 0x43000000, v152
	v_mul_f32_e32 v153, 0x43000000, v153
	v_mul_f32_e32 v154, 0x43000000, v154
	v_mul_f32_e32 v155, 0x43000000, v155
	ds_write_b128 v5, v[152:155] offset:5120
	v_mul_f32_e32 v156, 0x43000000, v156
	v_mul_f32_e32 v157, 0x43000000, v157
	v_mul_f32_e32 v158, 0x43000000, v158
	v_mul_f32_e32 v159, 0x43000000, v159
	ds_write_b128 v5, v[156:159] offset:6144
	v_mul_f32_e32 v160, 0x43000000, v160
	v_mul_f32_e32 v161, 0x43000000, v161
	v_mul_f32_e32 v162, 0x43000000, v162
	v_mul_f32_e32 v163, 0x43000000, v163
	ds_write_b128 v5, v[160:163] offset:7168
	s_waitcnt lgkmcnt(0)
	s_barrier
; #define GAS __attribute__((address_space(1)))
; #define LAS __attribute__((address_space(3)))
; #define LDS_WAIT() asm volatile("s_waitcnt lgkmcnt(0)" ::: "memory")
;     const int pr = item >> 1, kb = 2 * (pr / nblk) + (item & 1), nb = pr % nblk, k0 = 64 * kb, n0 = 32 * nb;
;     const int nr = n0 + (lane & 31); const int sc = MAP == 1 ? src_col_in(nr) : nr;
;     float v[32];
; #pragma unroll
;     for (int i = 0; i < 32; ++i) v[i] = sc >= 0 ? W[(size_t)(k0 + 2 * i + (lane >> 5)) * Nsrc + sc] : 0.f;
; #pragma unroll
;     for (int i = 0; i < 32; ++i) { const int k = k0 + 2 * i + (lane >> 5); float x = v[i] * wscale; if (KS) x *= (k < ksplit ? ksA[k] : ksB[k - ksplit]); scr[(2 * i + (lane >> 5)) * 33 + (lane & 31)] = x; }
;     LDS_WAIT(); asm volatile("" ::: "memory");
;     const int c = lane & 7;
; #pragma unroll
;     for (int j = 0; j < 4; ++j) { const int n = (lane >> 3) + 8 * j; const LAS float* s = scr + (8 * c) * 33 + n;
;         const unsigned long long o = (unsigned long long)pg8::pk4_fp8(s[0 * 33], s[1 * 33], s[2 * 33], s[3 * 33]) | ((unsigned long long)pg8::pk4_fp8(s[4 * 33], s[5 * 33], s[6 * 33], s[7 * 33]) << 32);
;         *(GAS unsigned long long*)(WT + (size_t)(n0 + n) * K + k0 + 8 * c) = o; }
;     LDS_WAIT(); asm volatile("" ::: "memory");
; }
; __global__ void __launch_bounds__(NWAVES * 64, 2) hybrid_fwd(Args args) {
;     ...
;             p0_transpose_item_f8<false>(args.in[16] + (size_t)l * FF * DM, FF, DM, DM / 32, (unsigned char*)(ws + WS_WDN + l * SZ_WDN), 128.f, args.in[16], args.in[16], 0, scr, r, lane);
	s_add_i32 s17, s16, 3744
	s_min_u32 s17, s17, 0xfff
	s_lshr_b32 s18, s17, 5
	s_add_i32 s18, s18, 0
	s_and_b32 s19, s17, 31
	s_lshl_b32 s18, s18, 21
	s_lshl_b32 s19, s19, 9
	s_add_u32 s18, s18, s19
	s_add_u32 s12, s2, s18
	s_addc_u32 s13, s3, 0
	global_load_dwordx4 v[132:135], v10, s[12:13]
	s_add_u32 s12, s12, 0x8000
	s_addc_u32 s13, s13, 0
	global_load_dwordx4 v[136:139], v10, s[12:13]
	s_add_u32 s12, s12, 0x8000
	s_addc_u32 s13, s13, 0
	global_load_dwordx4 v[140:143], v10, s[12:13]
	s_add_u32 s12, s12, 0x8000
	s_addc_u32 s13, s13, 0
	global_load_dwordx4 v[144:147], v10, s[12:13]
	s_add_u32 s12, s12, 0x8000
	s_addc_u32 s13, s13, 0
	global_load_dwordx4 v[148:151], v10, s[12:13]
	s_add_u32 s12, s12, 0x8000
	s_addc_u32 s13, s13, 0
	global_load_dwordx4 v[152:155], v10, s[12:13]
	s_add_u32 s12, s12, 0x8000
	s_addc_u32 s13, s13, 0
	global_load_dwordx4 v[156:159], v10, s[12:13]
	s_add_u32 s12, s12, 0x8000
	s_addc_u32 s13, s13, 0
	global_load_dwordx4 v[160:163], v10, s[12:13]
	s_add_i32 s17, s16, 3360
	s_min_u32 s17, s17, 0xfff
	s_lshr_b32 s18, s17, 5
	s_add_i32 s18, s18, 0
	s_and_b32 s19, s17, 31
	s_lshl_b32 s19, s19, 21
	s_lshl_b32 s18, s18, 7
	s_add_u32 s18, s18, s19
	s_add_u32 s14, s4, s18
	s_addc_u32 s15, s5, 0
	ds_read_b32 v170, v7
	ds_read_b32 v171, v7 offset:512
	ds_read_b32 v172, v7 offset:1024
	ds_read_b32 v173, v7 offset:1536
	ds_read_b32 v174, v7 offset:2048
	ds_read_b32 v175, v7 offset:2560
	ds_read_b32 v176, v7 offset:3072
	ds_read_b32 v177, v7 offset:3584
	ds_read_b32 v196, v7 offset:4096
	ds_read_b32 v197, v7 offset:4608
	ds_read_b32 v198, v7 offset:5120
	ds_read_b32 v199, v7 offset:5632
	ds_read_b32 v200, v7 offset:6144
	ds_read_b32 v201, v7 offset:6656
	ds_read_b32 v202, v7 offset:7168
	ds_read_b32 v203, v7 offset:7680
	s_waitcnt lgkmcnt(0)
	v_max_f32_e32 v170, v170, v170
	v_max_f32_e32 v171, v171, v171
	v_max_f32_e32 v172, v172, v172
	v_max_f32_e32 v173, v173, v173
	v_max_f32_e32 v174, v174, v174
	v_max_f32_e32 v175, v175, v175
	v_max_f32_e32 v176, v176, v176
	v_max_f32_e32 v177, v177, v177
	v_max_f32_e32 v196, v196, v196
	v_max_f32_e32 v197, v197, v197
	v_max_f32_e32 v198, v198, v198
	v_max_f32_e32 v199, v199, v199
	v_max_f32_e32 v200, v200, v200
	v_max_f32_e32 v201, v201, v201
	v_max_f32_e32 v202, v202, v202
	v_max_f32_e32 v203, v203, v203
	v_med3_f32 v170, v170, s20, v13
	v_med3_f32 v171, v171, s20, v13
	v_med3_f32 v172, v172, s20, v13
	v_med3_f32 v173, v173, s20, v13
	v_med3_f32 v174, v174, s20, v13
	v_med3_f32 v175, v175, s20, v13
	v_med3_f32 v176, v176, s20, v13
	v_med3_f32 v177, v177, s20, v13
	v_med3_f32 v196, v196, s20, v13
	v_med3_f32 v197, v197, s20, v13
	v_med3_f32 v198, v198, s20, v13
	v_med3_f32 v199, v199, s20, v13
	v_med3_f32 v200, v200, s20, v13
	v_med3_f32 v201, v201, s20, v13
	v_med3_f32 v202, v202, s20, v13
	v_med3_f32 v203, v203, s20, v13
	v_mov_b32_e32 v208, 0
	v_mov_b32_e32 v209, 0
	v_mov_b32_e32 v210, 0
	v_mov_b32_e32 v211, 0
	v_cvt_pk_fp8_f32 v208, v170, v171
	v_cvt_pk_fp8_f32 v209, v174, v175
	v_cvt_pk_fp8_f32 v210, v196, v197
	v_cvt_pk_fp8_f32 v211, v200, v201
	v_cvt_pk_fp8_f32 v208, v172, v173 op_sel:[0,0,1]
	v_cvt_pk_fp8_f32 v209, v176, v177 op_sel:[0,0,1]
	v_cvt_pk_fp8_f32 v210, v198, v199 op_sel:[0,0,1]
	v_cvt_pk_fp8_f32 v211, v202, v203 op_sel:[0,0,1]
	s_nop 0
	global_store_dwordx4 v11, v[208:211], s[14:15]
	ds_read_b32 v170, v9
	ds_read_b32 v171, v9 offset:512
	ds_read_b32 v172, v9 offset:1024
	ds_read_b32 v173, v9 offset:1536
	ds_read_b32 v174, v9 offset:2048
	ds_read_b32 v175, v9 offset:2560
	ds_read_b32 v176, v9 offset:3072
	ds_read_b32 v177, v9 offset:3584
	ds_read_b32 v196, v9 offset:4096
	ds_read_b32 v197, v9 offset:4608
	ds_read_b32 v198, v9 offset:5120
	ds_read_b32 v199, v9 offset:5632
	ds_read_b32 v200, v9 offset:6144
	ds_read_b32 v201, v9 offset:6656
	ds_read_b32 v202, v9 offset:7168
	ds_read_b32 v203, v9 offset:7680
	s_waitcnt lgkmcnt(0)
	v_max_f32_e32 v170, v170, v170
	v_max_f32_e32 v171, v171, v171
	v_max_f32_e32 v172, v172, v172
	v_max_f32_e32 v173, v173, v173
	v_max_f32_e32 v174, v174, v174
	v_max_f32_e32 v175, v175, v175
	v_max_f32_e32 v176, v176, v176
	v_max_f32_e32 v177, v177, v177
	v_max_f32_e32 v196, v196, v196
	v_max_f32_e32 v197, v197, v197
	v_max_f32_e32 v198, v198, v198
	v_max_f32_e32 v199, v199, v199
	v_max_f32_e32 v200, v200, v200
	v_max_f32_e32 v201, v201, v201
	v_max_f32_e32 v202, v202, v202
	v_max_f32_e32 v203, v203, v203
	v_med3_f32 v170, v170, s20, v13
	v_med3_f32 v171, v171, s20, v13
	v_med3_f32 v172, v172, s20, v13
	v_med3_f32 v173, v173, s20, v13
	v_med3_f32 v174, v174, s20, v13
	v_med3_f32 v175, v175, s20, v13
	v_med3_f32 v176, v176, s20, v13
	v_med3_f32 v177, v177, s20, v13
	v_med3_f32 v196, v196, s20, v13
	v_med3_f32 v197, v197, s20, v13
	v_med3_f32 v198, v198, s20, v13
	v_med3_f32 v199, v199, s20, v13
	v_med3_f32 v200, v200, s20, v13
	v_med3_f32 v201, v201, s20, v13
	v_med3_f32 v202, v202, s20, v13
	v_med3_f32 v203, v203, s20, v13
	v_mov_b32_e32 v208, 0
	v_mov_b32_e32 v209, 0
	v_mov_b32_e32 v210, 0
	v_mov_b32_e32 v211, 0
	v_cvt_pk_fp8_f32 v208, v170, v171
	v_cvt_pk_fp8_f32 v209, v174, v175
	v_cvt_pk_fp8_f32 v210, v196, v197
	v_cvt_pk_fp8_f32 v211, v200, v201
	v_cvt_pk_fp8_f32 v208, v172, v173 op_sel:[0,0,1]
	v_cvt_pk_fp8_f32 v209, v176, v177 op_sel:[0,0,1]
	v_cvt_pk_fp8_f32 v210, v198, v199 op_sel:[0,0,1]
	v_cvt_pk_fp8_f32 v211, v202, v203 op_sel:[0,0,1]
	s_nop 0
	global_store_dwordx4 v12, v[208:211], s[14:15]
	s_waitcnt vmcnt(32)
	v_mul_f32_e32 v36, 0x43000000, v36
	v_mul_f32_e32 v37, 0x43000000, v37
	v_mul_f32_e32 v38, 0x43000000, v38
	v_mul_f32_e32 v39, 0x43000000, v39
	ds_write_b128 v4, v[36:39]
	v_mul_f32_e32 v40, 0x43000000, v40
	v_mul_f32_e32 v41, 0x43000000, v41
	v_mul_f32_e32 v42, 0x43000000, v42
	v_mul_f32_e32 v43, 0x43000000, v43
	ds_write_b128 v4, v[40:43] offset:1024
	v_mul_f32_e32 v44, 0x43000000, v44
	v_mul_f32_e32 v45, 0x43000000, v45
	v_mul_f32_e32 v46, 0x43000000, v46
	v_mul_f32_e32 v47, 0x43000000, v47
	ds_write_b128 v4, v[44:47] offset:2048
	v_mul_f32_e32 v48, 0x43000000, v48
	v_mul_f32_e32 v49, 0x43000000, v49
	v_mul_f32_e32 v50, 0x43000000, v50
	v_mul_f32_e32 v51, 0x43000000, v51
	ds_write_b128 v4, v[48:51] offset:3072
	v_mul_f32_e32 v52, 0x43000000, v52
	v_mul_f32_e32 v53, 0x43000000, v53
	v_mul_f32_e32 v54, 0x43000000, v54
	v_mul_f32_e32 v55, 0x43000000, v55
	ds_write_b128 v4, v[52:55] offset:4096
	v_mul_f32_e32 v56, 0x43000000, v56
	v_mul_f32_e32 v57, 0x43000000, v57
	v_mul_f32_e32 v58, 0x43000000, v58
	v_mul_f32_e32 v59, 0x43000000, v59
	ds_write_b128 v4, v[56:59] offset:5120
	v_mul_f32_e32 v60, 0x43000000, v60
	v_mul_f32_e32 v61, 0x43000000, v61
	v_mul_f32_e32 v62, 0x43000000, v62
	v_mul_f32_e32 v63, 0x43000000, v63
	ds_write_b128 v4, v[60:63] offset:6144
	v_mul_f32_e32 v64, 0x43000000, v64
	v_mul_f32_e32 v65, 0x43000000, v65
	v_mul_f32_e32 v66, 0x43000000, v66
	v_mul_f32_e32 v67, 0x43000000, v67
	ds_write_b128 v4, v[64:67] offset:7168
	s_waitcnt lgkmcnt(0)
	s_barrier
; #define GAS __attribute__((address_space(1)))
; #define LAS __attribute__((address_space(3)))
; #define LDS_WAIT() asm volatile("s_waitcnt lgkmcnt(0)" ::: "memory")
;     const int pr = item >> 1, kb = 2 * (pr / nblk) + (item & 1), nb = pr % nblk, k0 = 64 * kb, n0 = 32 * nb;
;     const int nr = n0 + (lane & 31); const int sc = MAP == 1 ? src_col_in(nr) : nr;
;     float v[32];
; #pragma unroll
;     for (int i = 0; i < 32; ++i) v[i] = sc >= 0 ? W[(size_t)(k0 + 2 * i + (lane >> 5)) * Nsrc + sc] : 0.f;
; #pragma unroll
;     for (int i = 0; i < 32; ++i) { const int k = k0 + 2 * i + (lane >> 5); float x = v[i] * wscale; if (KS) x *= (k < ksplit ? ksA[k] : ksB[k - ksplit]); scr[(2 * i + (lane >> 5)) * 33 + (lane & 31)] = x; }
;     LDS_WAIT(); asm volatile("" ::: "memory");
;     const int c = lane & 7;
; #pragma unroll
;     for (int j = 0; j < 4; ++j) { const int n = (lane >> 3) + 8 * j; const LAS float* s = scr + (8 * c) * 33 + n;
;         const unsigned long long o = (unsigned long long)pg8::pk4_fp8(s[0 * 33], s[1 * 33], s[2 * 33], s[3 * 33]) | ((unsigned long long)pg8::pk4_fp8(s[4 * 33], s[5 * 33], s[6 * 33], s[7 * 33]) << 32);
;         *(GAS unsigned long long*)(WT + (size_t)(n0 + n) * K + k0 + 8 * c) = o; }
;     LDS_WAIT(); asm volatile("" ::: "memory");
; }
; __global__ void __launch_bounds__(NWAVES * 64, 2) hybrid_fwd(Args args) {
;     ...
;             p0_transpose_item_f8<false>(args.in[16] + (size_t)l * FF * DM, FF, DM, DM / 32, (unsigned char*)(ws + WS_WDN + l * SZ_WDN), 128.f, args.in[16], args.in[16], 0, scr, r, lane);
	s_add_i32 s17, s16, 3840
	s_min_u32 s17, s17, 0xfff
	s_lshr_b32 s18, s17, 5
	s_add_i32 s18, s18, 0
	s_and_b32 s19, s17, 31
	s_lshl_b32 s18, s18, 21
	s_lshl_b32 s19, s19, 9
	s_add_u32 s18, s18, s19
	s_add_u32 s12, s2, s18
	s_addc_u32 s13, s3, 0
	global_load_dwordx4 v[36:39], v10, s[12:13]
	s_add_u32 s12, s12, 0x8000
	s_addc_u32 s13, s13, 0
	global_load_dwordx4 v[40:43], v10, s[12:13]
	s_add_u32 s12, s12, 0x8000
	s_addc_u32 s13, s13, 0
	global_load_dwordx4 v[44:47], v10, s[12:13]
	s_add_u32 s12, s12, 0x8000
	s_addc_u32 s13, s13, 0
	global_load_dwordx4 v[48:51], v10, s[12:13]
	s_add_u32 s12, s12, 0x8000
	s_addc_u32 s13, s13, 0
	global_load_dwordx4 v[52:55], v10, s[12:13]
	s_add_u32 s12, s12, 0x8000
	s_addc_u32 s13, s13, 0
	global_load_dwordx4 v[56:59], v10, s[12:13]
	s_add_u32 s12, s12, 0x8000
	s_addc_u32 s13, s13, 0
	global_load_dwordx4 v[60:63], v10, s[12:13]
	s_add_u32 s12, s12, 0x8000
	s_addc_u32 s13, s13, 0
	global_load_dwordx4 v[64:67], v10, s[12:13]
	s_add_i32 s17, s16, 3456
	s_min_u32 s17, s17, 0xfff
	s_lshr_b32 s18, s17, 5
	s_add_i32 s18, s18, 0
	s_and_b32 s19, s17, 31
	s_lshl_b32 s19, s19, 21
	s_lshl_b32 s18, s18, 7
	s_add_u32 s18, s18, s19
	s_add_u32 s14, s4, s18
	s_addc_u32 s15, s5, 0
	ds_read_b32 v170, v6
	ds_read_b32 v171, v6 offset:512
	ds_read_b32 v172, v6 offset:1024
	ds_read_b32 v173, v6 offset:1536
	ds_read_b32 v174, v6 offset:2048
	ds_read_b32 v175, v6 offset:2560
	ds_read_b32 v176, v6 offset:3072
	ds_read_b32 v177, v6 offset:3584
	ds_read_b32 v196, v6 offset:4096
	ds_read_b32 v197, v6 offset:4608
	ds_read_b32 v198, v6 offset:5120
	ds_read_b32 v199, v6 offset:5632
	ds_read_b32 v200, v6 offset:6144
	ds_read_b32 v201, v6 offset:6656
	ds_read_b32 v202, v6 offset:7168
	ds_read_b32 v203, v6 offset:7680
	s_waitcnt lgkmcnt(0)
	v_max_f32_e32 v170, v170, v170
	v_max_f32_e32 v171, v171, v171
	v_max_f32_e32 v172, v172, v172
	v_max_f32_e32 v173, v173, v173
	v_max_f32_e32 v174, v174, v174
	v_max_f32_e32 v175, v175, v175
	v_max_f32_e32 v176, v176, v176
	v_max_f32_e32 v177, v177, v177
	v_max_f32_e32 v196, v196, v196
	v_max_f32_e32 v197, v197, v197
	v_max_f32_e32 v198, v198, v198
	v_max_f32_e32 v199, v199, v199
	v_max_f32_e32 v200, v200, v200
	v_max_f32_e32 v201, v201, v201
	v_max_f32_e32 v202, v202, v202
	v_max_f32_e32 v203, v203, v203
	v_med3_f32 v170, v170, s20, v13
	v_med3_f32 v171, v171, s20, v13
	v_med3_f32 v172, v172, s20, v13
	v_med3_f32 v173, v173, s20, v13
	v_med3_f32 v174, v174, s20, v13
	v_med3_f32 v175, v175, s20, v13
	v_med3_f32 v176, v176, s20, v13
	v_med3_f32 v177, v177, s20, v13
	v_med3_f32 v196, v196, s20, v13
	v_med3_f32 v197, v197, s20, v13
	v_med3_f32 v198, v198, s20, v13
	v_med3_f32 v199, v199, s20, v13
	v_med3_f32 v200, v200, s20, v13
	v_med3_f32 v201, v201, s20, v13
	v_med3_f32 v202, v202, s20, v13
	v_med3_f32 v203, v203, s20, v13
	v_mov_b32_e32 v208, 0
	v_mov_b32_e32 v209, 0
	v_mov_b32_e32 v210, 0
	v_mov_b32_e32 v211, 0
	v_cvt_pk_fp8_f32 v208, v170, v171
	v_cvt_pk_fp8_f32 v209, v174, v175
	v_cvt_pk_fp8_f32 v210, v196, v197
	v_cvt_pk_fp8_f32 v211, v200, v201
	v_cvt_pk_fp8_f32 v208, v172, v173 op_sel:[0,0,1]
	v_cvt_pk_fp8_f32 v209, v176, v177 op_sel:[0,0,1]
	v_cvt_pk_fp8_f32 v210, v198, v199 op_sel:[0,0,1]
	v_cvt_pk_fp8_f32 v211, v202, v203 op_sel:[0,0,1]
	s_nop 0
	global_store_dwordx4 v11, v[208:211], s[14:15]
	ds_read_b32 v170, v8
	ds_read_b32 v171, v8 offset:512
	ds_read_b32 v172, v8 offset:1024
	ds_read_b32 v173, v8 offset:1536
	ds_read_b32 v174, v8 offset:2048
	ds_read_b32 v175, v8 offset:2560
	ds_read_b32 v176, v8 offset:3072
	ds_read_b32 v177, v8 offset:3584
	ds_read_b32 v196, v8 offset:4096
	ds_read_b32 v197, v8 offset:4608
	ds_read_b32 v198, v8 offset:5120
	ds_read_b32 v199, v8 offset:5632
	ds_read_b32 v200, v8 offset:6144
	ds_read_b32 v201, v8 offset:6656
	ds_read_b32 v202, v8 offset:7168
	ds_read_b32 v203, v8 offset:7680
	s_waitcnt lgkmcnt(0)
	v_max_f32_e32 v170, v170, v170
	v_max_f32_e32 v171, v171, v171
	v_max_f32_e32 v172, v172, v172
	v_max_f32_e32 v173, v173, v173
	v_max_f32_e32 v174, v174, v174
	v_max_f32_e32 v175, v175, v175
	v_max_f32_e32 v176, v176, v176
	v_max_f32_e32 v177, v177, v177
	v_max_f32_e32 v196, v196, v196
	v_max_f32_e32 v197, v197, v197
	v_max_f32_e32 v198, v198, v198
	v_max_f32_e32 v199, v199, v199
	v_max_f32_e32 v200, v200, v200
	v_max_f32_e32 v201, v201, v201
	v_max_f32_e32 v202, v202, v202
	v_max_f32_e32 v203, v203, v203
	v_med3_f32 v170, v170, s20, v13
	v_med3_f32 v171, v171, s20, v13
	v_med3_f32 v172, v172, s20, v13
	v_med3_f32 v173, v173, s20, v13
	v_med3_f32 v174, v174, s20, v13
	v_med3_f32 v175, v175, s20, v13
	v_med3_f32 v176, v176, s20, v13
	v_med3_f32 v177, v177, s20, v13
	v_med3_f32 v196, v196, s20, v13
	v_med3_f32 v197, v197, s20, v13
	v_med3_f32 v198, v198, s20, v13
	v_med3_f32 v199, v199, s20, v13
	v_med3_f32 v200, v200, s20, v13
	v_med3_f32 v201, v201, s20, v13
	v_med3_f32 v202, v202, s20, v13
	v_med3_f32 v203, v203, s20, v13
	v_mov_b32_e32 v208, 0
	v_mov_b32_e32 v209, 0
	v_mov_b32_e32 v210, 0
	v_mov_b32_e32 v211, 0
	v_cvt_pk_fp8_f32 v208, v170, v171
	v_cvt_pk_fp8_f32 v209, v174, v175
	v_cvt_pk_fp8_f32 v210, v196, v197
	v_cvt_pk_fp8_f32 v211, v200, v201
	v_cvt_pk_fp8_f32 v208, v172, v173 op_sel:[0,0,1]
	v_cvt_pk_fp8_f32 v209, v176, v177 op_sel:[0,0,1]
	v_cvt_pk_fp8_f32 v210, v198, v199 op_sel:[0,0,1]
	v_cvt_pk_fp8_f32 v211, v202, v203 op_sel:[0,0,1]
	s_nop 0
	global_store_dwordx4 v12, v[208:211], s[14:15]
	s_waitcnt vmcnt(32)
	v_mul_f32_e32 v68, 0x43000000, v68
	v_mul_f32_e32 v69, 0x43000000, v69
	v_mul_f32_e32 v70, 0x43000000, v70
	v_mul_f32_e32 v71, 0x43000000, v71
	ds_write_b128 v5, v[68:71]
	v_mul_f32_e32 v72, 0x43000000, v72
	v_mul_f32_e32 v73, 0x43000000, v73
	v_mul_f32_e32 v74, 0x43000000, v74
	v_mul_f32_e32 v75, 0x43000000, v75
	ds_write_b128 v5, v[72:75] offset:1024
	v_mul_f32_e32 v76, 0x43000000, v76
	v_mul_f32_e32 v77, 0x43000000, v77
	v_mul_f32_e32 v78, 0x43000000, v78
	v_mul_f32_e32 v79, 0x43000000, v79
	ds_write_b128 v5, v[76:79] offset:2048
	v_mul_f32_e32 v80, 0x43000000, v80
	v_mul_f32_e32 v81, 0x43000000, v81
	v_mul_f32_e32 v82, 0x43000000, v82
	v_mul_f32_e32 v83, 0x43000000, v83
	ds_write_b128 v5, v[80:83] offset:3072
	v_mul_f32_e32 v84, 0x43000000, v84
	v_mul_f32_e32 v85, 0x43000000, v85
	v_mul_f32_e32 v86, 0x43000000, v86
	v_mul_f32_e32 v87, 0x43000000, v87
	ds_write_b128 v5, v[84:87] offset:4096
	v_mul_f32_e32 v88, 0x43000000, v88
	v_mul_f32_e32 v89, 0x43000000, v89
	v_mul_f32_e32 v90, 0x43000000, v90
	v_mul_f32_e32 v91, 0x43000000, v91
	ds_write_b128 v5, v[88:91] offset:5120
	v_mul_f32_e32 v92, 0x43000000, v92
	v_mul_f32_e32 v93, 0x43000000, v93
	v_mul_f32_e32 v94, 0x43000000, v94
	v_mul_f32_e32 v95, 0x43000000, v95
	ds_write_b128 v5, v[92:95] offset:6144
	v_mul_f32_e32 v96, 0x43000000, v96
	v_mul_f32_e32 v97, 0x43000000, v97
	v_mul_f32_e32 v98, 0x43000000, v98
	v_mul_f32_e32 v99, 0x43000000, v99
	ds_write_b128 v5, v[96:99] offset:7168
	s_waitcnt lgkmcnt(0)
	s_barrier
; #define GAS __attribute__((address_space(1)))
; #define LAS __attribute__((address_space(3)))
; #define LDS_WAIT() asm volatile("s_waitcnt lgkmcnt(0)" ::: "memory")
;     const int pr = item >> 1, kb = 2 * (pr / nblk) + (item & 1), nb = pr % nblk, k0 = 64 * kb, n0 = 32 * nb;
;     const int nr = n0 + (lane & 31); const int sc = MAP == 1 ? src_col_in(nr) : nr;
;     float v[32];
; #pragma unroll
;     for (int i = 0; i < 32; ++i) v[i] = sc >= 0 ? W[(size_t)(k0 + 2 * i + (lane >> 5)) * Nsrc + sc] : 0.f;
; #pragma unroll
;     for (int i = 0; i < 32; ++i) { const int k = k0 + 2 * i + (lane >> 5); float x = v[i] * wscale; if (KS) x *= (k < ksplit ? ksA[k] : ksB[k - ksplit]); scr[(2 * i + (lane >> 5)) * 33 + (lane & 31)] = x; }
;     LDS_WAIT(); asm volatile("" ::: "memory");
;     const int c = lane & 7;
; #pragma unroll
;     for (int j = 0; j < 4; ++j) { const int n = (lane >> 3) + 8 * j; const LAS float* s = scr + (8 * c) * 33 + n;
;         const unsigned long long o = (unsigned long long)pg8::pk4_fp8(s[0 * 33], s[1 * 33], s[2 * 33], s[3 * 33]) | ((unsigned long long)pg8::pk4_fp8(s[4 * 33], s[5 * 33], s[6 * 33], s[7 * 33]) << 32);
;         *(GAS unsigned long long*)(WT + (size_t)(n0 + n) * K + k0 + 8 * c) = o; }
;     LDS_WAIT(); asm volatile("" ::: "memory");
; }
; __global__ void __launch_bounds__(NWAVES * 64, 2) hybrid_fwd(Args args) {
;     ...
;             p0_transpose_item_f8<false>(args.in[16] + (size_t)l * FF * DM, FF, DM, DM / 32, (unsigned char*)(ws + WS_WDN + l * SZ_WDN), 128.f, args.in[16], args.in[16], 0, scr, r, lane);
	s_add_i32 s17, s16, 3936
	s_min_u32 s17, s17, 0xfff
	s_lshr_b32 s18, s17, 5
	s_add_i32 s18, s18, 0
	s_and_b32 s19, s17, 31
	s_lshl_b32 s18, s18, 21
	s_lshl_b32 s19, s19, 9
	s_add_u32 s18, s18, s19
	s_add_u32 s12, s2, s18
	s_addc_u32 s13, s3, 0
	global_load_dwordx4 v[68:71], v10, s[12:13]
	s_add_u32 s12, s12, 0x8000
	s_addc_u32 s13, s13, 0
	global_load_dwordx4 v[72:75], v10, s[12:13]
	s_add_u32 s12, s12, 0x8000
	s_addc_u32 s13, s13, 0
	global_load_dwordx4 v[76:79], v10, s[12:13]
	s_add_u32 s12, s12, 0x8000
	s_addc_u32 s13, s13, 0
	global_load_dwordx4 v[80:83], v10, s[12:13]
	s_add_u32 s12, s12, 0x8000
	s_addc_u32 s13, s13, 0
	global_load_dwordx4 v[84:87], v10, s[12:13]
	s_add_u32 s12, s12, 0x8000
	s_addc_u32 s13, s13, 0
	global_load_dwordx4 v[88:91], v10, s[12:13]
	s_add_u32 s12, s12, 0x8000
	s_addc_u32 s13, s13, 0
	global_load_dwordx4 v[92:95], v10, s[12:13]
	s_add_u32 s12, s12, 0x8000
	s_addc_u32 s13, s13, 0
	global_load_dwordx4 v[96:99], v10, s[12:13]
	s_add_i32 s17, s16, 3552
	s_min_u32 s17, s17, 0xfff
	s_lshr_b32 s18, s17, 5
	s_add_i32 s18, s18, 0
	s_and_b32 s19, s17, 31
	s_lshl_b32 s19, s19, 21
	s_lshl_b32 s18, s18, 7
	s_add_u32 s18, s18, s19
	s_add_u32 s14, s4, s18
	s_addc_u32 s15, s5, 0
	ds_read_b32 v170, v7
	ds_read_b32 v171, v7 offset:512
	ds_read_b32 v172, v7 offset:1024
	ds_read_b32 v173, v7 offset:1536
	ds_read_b32 v174, v7 offset:2048
	ds_read_b32 v175, v7 offset:2560
	ds_read_b32 v176, v7 offset:3072
	ds_read_b32 v177, v7 offset:3584
	ds_read_b32 v196, v7 offset:4096
	ds_read_b32 v197, v7 offset:4608
	ds_read_b32 v198, v7 offset:5120
	ds_read_b32 v199, v7 offset:5632
	ds_read_b32 v200, v7 offset:6144
	ds_read_b32 v201, v7 offset:6656
	ds_read_b32 v202, v7 offset:7168
	ds_read_b32 v203, v7 offset:7680
	s_waitcnt lgkmcnt(0)
	v_max_f32_e32 v170, v170, v170
	v_max_f32_e32 v171, v171, v171
	v_max_f32_e32 v172, v172, v172
	v_max_f32_e32 v173, v173, v173
	v_max_f32_e32 v174, v174, v174
	v_max_f32_e32 v175, v175, v175
	v_max_f32_e32 v176, v176, v176
	v_max_f32_e32 v177, v177, v177
	v_max_f32_e32 v196, v196, v196
	v_max_f32_e32 v197, v197, v197
	v_max_f32_e32 v198, v198, v198
	v_max_f32_e32 v199, v199, v199
	v_max_f32_e32 v200, v200, v200
	v_max_f32_e32 v201, v201, v201
	v_max_f32_e32 v202, v202, v202
	v_max_f32_e32 v203, v203, v203
	v_med3_f32 v170, v170, s20, v13
	v_med3_f32 v171, v171, s20, v13
	v_med3_f32 v172, v172, s20, v13
	v_med3_f32 v173, v173, s20, v13
	v_med3_f32 v174, v174, s20, v13
	v_med3_f32 v175, v175, s20, v13
	v_med3_f32 v176, v176, s20, v13
	v_med3_f32 v177, v177, s20, v13
	v_med3_f32 v196, v196, s20, v13
	v_med3_f32 v197, v197, s20, v13
	v_med3_f32 v198, v198, s20, v13
	v_med3_f32 v199, v199, s20, v13
	v_med3_f32 v200, v200, s20, v13
	v_med3_f32 v201, v201, s20, v13
	v_med3_f32 v202, v202, s20, v13
	v_med3_f32 v203, v203, s20, v13
	v_mov_b32_e32 v208, 0
	v_mov_b32_e32 v209, 0
	v_mov_b32_e32 v210, 0
	v_mov_b32_e32 v211, 0
	v_cvt_pk_fp8_f32 v208, v170, v171
	v_cvt_pk_fp8_f32 v209, v174, v175
	v_cvt_pk_fp8_f32 v210, v196, v197
	v_cvt_pk_fp8_f32 v211, v200, v201
	v_cvt_pk_fp8_f32 v208, v172, v173 op_sel:[0,0,1]
	v_cvt_pk_fp8_f32 v209, v176, v177 op_sel:[0,0,1]
	v_cvt_pk_fp8_f32 v210, v198, v199 op_sel:[0,0,1]
	v_cvt_pk_fp8_f32 v211, v202, v203 op_sel:[0,0,1]
	s_nop 0
	global_store_dwordx4 v11, v[208:211], s[14:15]
	ds_read_b32 v170, v9
	ds_read_b32 v171, v9 offset:512
	ds_read_b32 v172, v9 offset:1024
	ds_read_b32 v173, v9 offset:1536
	ds_read_b32 v174, v9 offset:2048
	ds_read_b32 v175, v9 offset:2560
	ds_read_b32 v176, v9 offset:3072
	ds_read_b32 v177, v9 offset:3584
	ds_read_b32 v196, v9 offset:4096
	ds_read_b32 v197, v9 offset:4608
	ds_read_b32 v198, v9 offset:5120
	ds_read_b32 v199, v9 offset:5632
	ds_read_b32 v200, v9 offset:6144
	ds_read_b32 v201, v9 offset:6656
	ds_read_b32 v202, v9 offset:7168
	ds_read_b32 v203, v9 offset:7680
	s_waitcnt lgkmcnt(0)
	v_max_f32_e32 v170, v170, v170
	v_max_f32_e32 v171, v171, v171
	v_max_f32_e32 v172, v172, v172
	v_max_f32_e32 v173, v173, v173
	v_max_f32_e32 v174, v174, v174
	v_max_f32_e32 v175, v175, v175
	v_max_f32_e32 v176, v176, v176
	v_max_f32_e32 v177, v177, v177
	v_max_f32_e32 v196, v196, v196
	v_max_f32_e32 v197, v197, v197
	v_max_f32_e32 v198, v198, v198
	v_max_f32_e32 v199, v199, v199
	v_max_f32_e32 v200, v200, v200
	v_max_f32_e32 v201, v201, v201
	v_max_f32_e32 v202, v202, v202
	v_max_f32_e32 v203, v203, v203
	v_med3_f32 v170, v170, s20, v13
	v_med3_f32 v171, v171, s20, v13
	v_med3_f32 v172, v172, s20, v13
	v_med3_f32 v173, v173, s20, v13
	v_med3_f32 v174, v174, s20, v13
	v_med3_f32 v175, v175, s20, v13
	v_med3_f32 v176, v176, s20, v13
	v_med3_f32 v177, v177, s20, v13
	v_med3_f32 v196, v196, s20, v13
	v_med3_f32 v197, v197, s20, v13
	v_med3_f32 v198, v198, s20, v13
	v_med3_f32 v199, v199, s20, v13
	v_med3_f32 v200, v200, s20, v13
	v_med3_f32 v201, v201, s20, v13
	v_med3_f32 v202, v202, s20, v13
	v_med3_f32 v203, v203, s20, v13
	v_mov_b32_e32 v208, 0
	v_mov_b32_e32 v209, 0
	v_mov_b32_e32 v210, 0
	v_mov_b32_e32 v211, 0
	v_cvt_pk_fp8_f32 v208, v170, v171
	v_cvt_pk_fp8_f32 v209, v174, v175
	v_cvt_pk_fp8_f32 v210, v196, v197
	v_cvt_pk_fp8_f32 v211, v200, v201
	v_cvt_pk_fp8_f32 v208, v172, v173 op_sel:[0,0,1]
	v_cvt_pk_fp8_f32 v209, v176, v177 op_sel:[0,0,1]
	v_cvt_pk_fp8_f32 v210, v198, v199 op_sel:[0,0,1]
	v_cvt_pk_fp8_f32 v211, v202, v203 op_sel:[0,0,1]
	s_nop 0
	global_store_dwordx4 v12, v[208:211], s[14:15]
	s_waitcnt vmcnt(32)
	v_mul_f32_e32 v100, 0x43000000, v100
	v_mul_f32_e32 v101, 0x43000000, v101
	v_mul_f32_e32 v102, 0x43000000, v102
	v_mul_f32_e32 v103, 0x43000000, v103
	ds_write_b128 v4, v[100:103]
	v_mul_f32_e32 v104, 0x43000000, v104
	v_mul_f32_e32 v105, 0x43000000, v105
	v_mul_f32_e32 v106, 0x43000000, v106
	v_mul_f32_e32 v107, 0x43000000, v107
	ds_write_b128 v4, v[104:107] offset:1024
	v_mul_f32_e32 v108, 0x43000000, v108
	v_mul_f32_e32 v109, 0x43000000, v109
	v_mul_f32_e32 v110, 0x43000000, v110
	v_mul_f32_e32 v111, 0x43000000, v111
	ds_write_b128 v4, v[108:111] offset:2048
	v_mul_f32_e32 v112, 0x43000000, v112
	v_mul_f32_e32 v113, 0x43000000, v113
	v_mul_f32_e32 v114, 0x43000000, v114
	v_mul_f32_e32 v115, 0x43000000, v115
	ds_write_b128 v4, v[112:115] offset:3072
	v_mul_f32_e32 v116, 0x43000000, v116
	v_mul_f32_e32 v117, 0x43000000, v117
	v_mul_f32_e32 v118, 0x43000000, v118
	v_mul_f32_e32 v119, 0x43000000, v119
	ds_write_b128 v4, v[116:119] offset:4096
	v_mul_f32_e32 v120, 0x43000000, v120
	v_mul_f32_e32 v121, 0x43000000, v121
	v_mul_f32_e32 v122, 0x43000000, v122
	v_mul_f32_e32 v123, 0x43000000, v123
	ds_write_b128 v4, v[120:123] offset:5120
	v_mul_f32_e32 v124, 0x43000000, v124
	v_mul_f32_e32 v125, 0x43000000, v125
	v_mul_f32_e32 v126, 0x43000000, v126
	v_mul_f32_e32 v127, 0x43000000, v127
	ds_write_b128 v4, v[124:127] offset:6144
	v_mul_f32_e32 v128, 0x43000000, v128
	v_mul_f32_e32 v129, 0x43000000, v129
	v_mul_f32_e32 v130, 0x43000000, v130
	v_mul_f32_e32 v131, 0x43000000, v131
	ds_write_b128 v4, v[128:131] offset:7168
	s_waitcnt lgkmcnt(0)
	s_barrier
; #define GAS __attribute__((address_space(1)))
; #define LAS __attribute__((address_space(3)))
; #define LDS_WAIT() asm volatile("s_waitcnt lgkmcnt(0)" ::: "memory")
;     const int pr = item >> 1, kb = 2 * (pr / nblk) + (item & 1), nb = pr % nblk, k0 = 64 * kb, n0 = 32 * nb;
;     const int nr = n0 + (lane & 31); const int sc = MAP == 1 ? src_col_in(nr) : nr;
;     float v[32];
; #pragma unroll
;     for (int i = 0; i < 32; ++i) v[i] = sc >= 0 ? W[(size_t)(k0 + 2 * i + (lane >> 5)) * Nsrc + sc] : 0.f;
; #pragma unroll
;     for (int i = 0; i < 32; ++i) { const int k = k0 + 2 * i + (lane >> 5); float x = v[i] * wscale; if (KS) x *= (k < ksplit ? ksA[k] : ksB[k - ksplit]); scr[(2 * i + (lane >> 5)) * 33 + (lane & 31)] = x; }
;     LDS_WAIT(); asm volatile("" ::: "memory");
;     const int c = lane & 7;
; #pragma unroll
;     for (int j = 0; j < 4; ++j) { const int n = (lane >> 3) + 8 * j; const LAS float* s = scr + (8 * c) * 33 + n;
;         const unsigned long long o = (unsigned long long)pg8::pk4_fp8(s[0 * 33], s[1 * 33], s[2 * 33], s[3 * 33]) | ((unsigned long long)pg8::pk4_fp8(s[4 * 33], s[5 * 33], s[6 * 33], s[7 * 33]) << 32);
;         *(GAS unsigned long long*)(WT + (size_t)(n0 + n) * K + k0 + 8 * c) = o; }
;     LDS_WAIT(); asm volatile("" ::: "memory");
; }
; __global__ void __launch_bounds__(NWAVES * 64, 2) hybrid_fwd(Args args) {
;     ...
;             p0_transpose_item_f8<false>(args.in[16] + (size_t)l * FF * DM, FF, DM, DM / 32, (unsigned char*)(ws + WS_WDN + l * SZ_WDN), 128.f, args.in[16], args.in[16], 0, scr, r, lane);
	s_add_i32 s17, s16, 4032
	s_min_u32 s17, s17, 0xfff
	s_lshr_b32 s18, s17, 5
	s_add_i32 s18, s18, 0
	s_and_b32 s19, s17, 31
	s_lshl_b32 s18, s18, 21
	s_lshl_b32 s19, s19, 9
	s_add_u32 s18, s18, s19
	s_add_u32 s12, s2, s18
	s_addc_u32 s13, s3, 0
	global_load_dwordx4 v[100:103], v10, s[12:13]
	s_add_u32 s12, s12, 0x8000
	s_addc_u32 s13, s13, 0
	global_load_dwordx4 v[104:107], v10, s[12:13]
	s_add_u32 s12, s12, 0x8000
	s_addc_u32 s13, s13, 0
	global_load_dwordx4 v[108:111], v10, s[12:13]
	s_add_u32 s12, s12, 0x8000
	s_addc_u32 s13, s13, 0
	global_load_dwordx4 v[112:115], v10, s[12:13]
	s_add_u32 s12, s12, 0x8000
	s_addc_u32 s13, s13, 0
	global_load_dwordx4 v[116:119], v10, s[12:13]
	s_add_u32 s12, s12, 0x8000
	s_addc_u32 s13, s13, 0
	global_load_dwordx4 v[120:123], v10, s[12:13]
	s_add_u32 s12, s12, 0x8000
	s_addc_u32 s13, s13, 0
	global_load_dwordx4 v[124:127], v10, s[12:13]
	s_add_u32 s12, s12, 0x8000
	s_addc_u32 s13, s13, 0
	global_load_dwordx4 v[128:131], v10, s[12:13]
	s_add_i32 s17, s16, 3648
	s_min_u32 s17, s17, 0xfff
	s_lshr_b32 s18, s17, 5
	s_add_i32 s18, s18, 0
	s_and_b32 s19, s17, 31
	s_lshl_b32 s19, s19, 21
	s_lshl_b32 s18, s18, 7
	s_add_u32 s18, s18, s19
	s_add_u32 s14, s4, s18
	s_addc_u32 s15, s5, 0
	ds_read_b32 v170, v6
	ds_read_b32 v171, v6 offset:512
	ds_read_b32 v172, v6 offset:1024
	ds_read_b32 v173, v6 offset:1536
	ds_read_b32 v174, v6 offset:2048
	ds_read_b32 v175, v6 offset:2560
	ds_read_b32 v176, v6 offset:3072
	ds_read_b32 v177, v6 offset:3584
	ds_read_b32 v196, v6 offset:4096
	ds_read_b32 v197, v6 offset:4608
	ds_read_b32 v198, v6 offset:5120
	ds_read_b32 v199, v6 offset:5632
	ds_read_b32 v200, v6 offset:6144
	ds_read_b32 v201, v6 offset:6656
	ds_read_b32 v202, v6 offset:7168
	ds_read_b32 v203, v6 offset:7680
	s_waitcnt lgkmcnt(0)
	v_max_f32_e32 v170, v170, v170
	v_max_f32_e32 v171, v171, v171
	v_max_f32_e32 v172, v172, v172
	v_max_f32_e32 v173, v173, v173
	v_max_f32_e32 v174, v174, v174
	v_max_f32_e32 v175, v175, v175
	v_max_f32_e32 v176, v176, v176
	v_max_f32_e32 v177, v177, v177
	v_max_f32_e32 v196, v196, v196
	v_max_f32_e32 v197, v197, v197
	v_max_f32_e32 v198, v198, v198
	v_max_f32_e32 v199, v199, v199
	v_max_f32_e32 v200, v200, v200
	v_max_f32_e32 v201, v201, v201
	v_max_f32_e32 v202, v202, v202
	v_max_f32_e32 v203, v203, v203
	v_med3_f32 v170, v170, s20, v13
	v_med3_f32 v171, v171, s20, v13
	v_med3_f32 v172, v172, s20, v13
	v_med3_f32 v173, v173, s20, v13
	v_med3_f32 v174, v174, s20, v13
	v_med3_f32 v175, v175, s20, v13
	v_med3_f32 v176, v176, s20, v13
	v_med3_f32 v177, v177, s20, v13
	v_med3_f32 v196, v196, s20, v13
	v_med3_f32 v197, v197, s20, v13
	v_med3_f32 v198, v198, s20, v13
	v_med3_f32 v199, v199, s20, v13
	v_med3_f32 v200, v200, s20, v13
	v_med3_f32 v201, v201, s20, v13
	v_med3_f32 v202, v202, s20, v13
	v_med3_f32 v203, v203, s20, v13
	v_mov_b32_e32 v208, 0
	v_mov_b32_e32 v209, 0
	v_mov_b32_e32 v210, 0
	v_mov_b32_e32 v211, 0
	v_cvt_pk_fp8_f32 v208, v170, v171
	v_cvt_pk_fp8_f32 v209, v174, v175
	v_cvt_pk_fp8_f32 v210, v196, v197
	v_cvt_pk_fp8_f32 v211, v200, v201
	v_cvt_pk_fp8_f32 v208, v172, v173 op_sel:[0,0,1]
	v_cvt_pk_fp8_f32 v209, v176, v177 op_sel:[0,0,1]
	v_cvt_pk_fp8_f32 v210, v198, v199 op_sel:[0,0,1]
	v_cvt_pk_fp8_f32 v211, v202, v203 op_sel:[0,0,1]
	s_nop 0
	global_store_dwordx4 v11, v[208:211], s[14:15]
	ds_read_b32 v170, v8
	ds_read_b32 v171, v8 offset:512
	ds_read_b32 v172, v8 offset:1024
	ds_read_b32 v173, v8 offset:1536
	ds_read_b32 v174, v8 offset:2048
	ds_read_b32 v175, v8 offset:2560
	ds_read_b32 v176, v8 offset:3072
	ds_read_b32 v177, v8 offset:3584
	ds_read_b32 v196, v8 offset:4096
	ds_read_b32 v197, v8 offset:4608
	ds_read_b32 v198, v8 offset:5120
	ds_read_b32 v199, v8 offset:5632
	ds_read_b32 v200, v8 offset:6144
	ds_read_b32 v201, v8 offset:6656
	ds_read_b32 v202, v8 offset:7168
	ds_read_b32 v203, v8 offset:7680
	s_waitcnt lgkmcnt(0)
	v_max_f32_e32 v170, v170, v170
	v_max_f32_e32 v171, v171, v171
	v_max_f32_e32 v172, v172, v172
	v_max_f32_e32 v173, v173, v173
	v_max_f32_e32 v174, v174, v174
	v_max_f32_e32 v175, v175, v175
	v_max_f32_e32 v176, v176, v176
	v_max_f32_e32 v177, v177, v177
	v_max_f32_e32 v196, v196, v196
	v_max_f32_e32 v197, v197, v197
	v_max_f32_e32 v198, v198, v198
	v_max_f32_e32 v199, v199, v199
	v_max_f32_e32 v200, v200, v200
	v_max_f32_e32 v201, v201, v201
	v_max_f32_e32 v202, v202, v202
	v_max_f32_e32 v203, v203, v203
	v_med3_f32 v170, v170, s20, v13
	v_med3_f32 v171, v171, s20, v13
	v_med3_f32 v172, v172, s20, v13
	v_med3_f32 v173, v173, s20, v13
	v_med3_f32 v174, v174, s20, v13
	v_med3_f32 v175, v175, s20, v13
	v_med3_f32 v176, v176, s20, v13
	v_med3_f32 v177, v177, s20, v13
	v_med3_f32 v196, v196, s20, v13
	v_med3_f32 v197, v197, s20, v13
	v_med3_f32 v198, v198, s20, v13
	v_med3_f32 v199, v199, s20, v13
	v_med3_f32 v200, v200, s20, v13
	v_med3_f32 v201, v201, s20, v13
	v_med3_f32 v202, v202, s20, v13
	v_med3_f32 v203, v203, s20, v13
	v_mov_b32_e32 v208, 0
	v_mov_b32_e32 v209, 0
	v_mov_b32_e32 v210, 0
	v_mov_b32_e32 v211, 0
	v_cvt_pk_fp8_f32 v208, v170, v171
	v_cvt_pk_fp8_f32 v209, v174, v175
	v_cvt_pk_fp8_f32 v210, v196, v197
	v_cvt_pk_fp8_f32 v211, v200, v201
	v_cvt_pk_fp8_f32 v208, v172, v173 op_sel:[0,0,1]
	v_cvt_pk_fp8_f32 v209, v176, v177 op_sel:[0,0,1]
	v_cvt_pk_fp8_f32 v210, v198, v199 op_sel:[0,0,1]
	v_cvt_pk_fp8_f32 v211, v202, v203 op_sel:[0,0,1]
	s_nop 0
	global_store_dwordx4 v12, v[208:211], s[14:15]
	s_waitcnt vmcnt(32)
	v_mul_f32_e32 v132, 0x43000000, v132
	v_mul_f32_e32 v133, 0x43000000, v133
	v_mul_f32_e32 v134, 0x43000000, v134
	v_mul_f32_e32 v135, 0x43000000, v135
	ds_write_b128 v5, v[132:135]
	v_mul_f32_e32 v136, 0x43000000, v136
	v_mul_f32_e32 v137, 0x43000000, v137
	v_mul_f32_e32 v138, 0x43000000, v138
	v_mul_f32_e32 v139, 0x43000000, v139
	ds_write_b128 v5, v[136:139] offset:1024
	v_mul_f32_e32 v140, 0x43000000, v140
	v_mul_f32_e32 v141, 0x43000000, v141
	v_mul_f32_e32 v142, 0x43000000, v142
	v_mul_f32_e32 v143, 0x43000000, v143
	ds_write_b128 v5, v[140:143] offset:2048
	v_mul_f32_e32 v144, 0x43000000, v144
	v_mul_f32_e32 v145, 0x43000000, v145
	v_mul_f32_e32 v146, 0x43000000, v146
	v_mul_f32_e32 v147, 0x43000000, v147
	ds_write_b128 v5, v[144:147] offset:3072
	v_mul_f32_e32 v148, 0x43000000, v148
	v_mul_f32_e32 v149, 0x43000000, v149
	v_mul_f32_e32 v150, 0x43000000, v150
	v_mul_f32_e32 v151, 0x43000000, v151
	ds_write_b128 v5, v[148:151] offset:4096
	v_mul_f32_e32 v152, 0x43000000, v152
	v_mul_f32_e32 v153, 0x43000000, v153
	v_mul_f32_e32 v154, 0x43000000, v154
	v_mul_f32_e32 v155, 0x43000000, v155
	ds_write_b128 v5, v[152:155] offset:5120
	v_mul_f32_e32 v156, 0x43000000, v156
	v_mul_f32_e32 v157, 0x43000000, v157
	v_mul_f32_e32 v158, 0x43000000, v158
	v_mul_f32_e32 v159, 0x43000000, v159
	ds_write_b128 v5, v[156:159] offset:6144
	v_mul_f32_e32 v160, 0x43000000, v160
	v_mul_f32_e32 v161, 0x43000000, v161
	v_mul_f32_e32 v162, 0x43000000, v162
	v_mul_f32_e32 v163, 0x43000000, v163
	ds_write_b128 v5, v[160:163] offset:7168
	s_waitcnt lgkmcnt(0)
	s_barrier
; #define GAS __attribute__((address_space(1)))
; #define LAS __attribute__((address_space(3)))
; #define LDS_WAIT() asm volatile("s_waitcnt lgkmcnt(0)" ::: "memory")
;     const int pr = item >> 1, kb = 2 * (pr / nblk) + (item & 1), nb = pr % nblk, k0 = 64 * kb, n0 = 32 * nb;
;     const int nr = n0 + (lane & 31); const int sc = MAP == 1 ? src_col_in(nr) : nr;
;     float v[32];
; #pragma unroll
;     for (int i = 0; i < 32; ++i) v[i] = sc >= 0 ? W[(size_t)(k0 + 2 * i + (lane >> 5)) * Nsrc + sc] : 0.f;
; #pragma unroll
;     for (int i = 0; i < 32; ++i) { const int k = k0 + 2 * i + (lane >> 5); float x = v[i] * wscale; if (KS) x *= (k < ksplit ? ksA[k] : ksB[k - ksplit]); scr[(2 * i + (lane >> 5)) * 33 + (lane & 31)] = x; }
;     LDS_WAIT(); asm volatile("" ::: "memory");
;     const int c = lane & 7;
; #pragma unroll
;     for (int j = 0; j < 4; ++j) { const int n = (lane >> 3) + 8 * j; const LAS float* s = scr + (8 * c) * 33 + n;
;         const unsigned long long o = (unsigned long long)pg8::pk4_fp8(s[0 * 33], s[1 * 33], s[2 * 33], s[3 * 33]) | ((unsigned long long)pg8::pk4_fp8(s[4 * 33], s[5 * 33], s[6 * 33], s[7 * 33]) << 32);
;         *(GAS unsigned long long*)(WT + (size_t)(n0 + n) * K + k0 + 8 * c) = o; }
;     LDS_WAIT(); asm volatile("" ::: "memory");
; }
; __global__ void __launch_bounds__(NWAVES * 64, 2) hybrid_fwd(Args args) {
;     ...
;             if (r < I_O) { if (l >= WO_F8_FROM) p0_transpose_item_f8<true>(args.in[13] + (size_t)l * DM * DM, DM, DM, DM / 32, (unsigned char*)(ws + WS_WO + l * SZ_WO), 64.f, args.in[6] + l * 2048, args.in[12] + l * 2048, 2048, scr, r, lane);
	s_add_i32 s19, s39, 0
	s_min_u32 s19, s19, 31
	s_lshl_b32 s19, s19, 9
	s_add_u32 s12, s22, s19
	s_addc_u32 s13, s23, 0
	global_load_dwordx4 v[132:135], v10, s[12:13]
	s_add_u32 s12, s12, 0x8000
	s_addc_u32 s13, s13, 0
	global_load_dwordx4 v[136:139], v10, s[12:13]
	s_add_u32 s12, s12, 0x8000
	s_addc_u32 s13, s13, 0
	global_load_dwordx4 v[140:143], v10, s[12:13]
	s_add_u32 s12, s12, 0x8000
	s_addc_u32 s13, s13, 0
	global_load_dwordx4 v[144:147], v10, s[12:13]
	s_add_u32 s12, s12, 0x8000
	s_addc_u32 s13, s13, 0
	global_load_dwordx4 v[148:151], v10, s[12:13]
	s_add_u32 s12, s12, 0x8000
	s_addc_u32 s13, s13, 0
	global_load_dwordx4 v[152:155], v10, s[12:13]
	s_add_u32 s12, s12, 0x8000
	s_addc_u32 s13, s13, 0
	global_load_dwordx4 v[156:159], v10, s[12:13]
	s_add_u32 s12, s12, 0x8000
	s_addc_u32 s13, s13, 0
	global_load_dwordx4 v[160:163], v10, s[12:13]
	s_add_i32 s17, s16, 3744
	s_min_u32 s17, s17, 0xfff
	s_lshr_b32 s18, s17, 5
	s_add_i32 s18, s18, 0
	s_and_b32 s19, s17, 31
	s_lshl_b32 s19, s19, 21
	s_lshl_b32 s18, s18, 7
	s_add_u32 s18, s18, s19
	s_add_u32 s14, s4, s18
	s_addc_u32 s15, s5, 0
	ds_read_b32 v170, v7
	ds_read_b32 v171, v7 offset:512
	ds_read_b32 v172, v7 offset:1024
	ds_read_b32 v173, v7 offset:1536
	ds_read_b32 v174, v7 offset:2048
	ds_read_b32 v175, v7 offset:2560
	ds_read_b32 v176, v7 offset:3072
	ds_read_b32 v177, v7 offset:3584
	ds_read_b32 v196, v7 offset:4096
	ds_read_b32 v197, v7 offset:4608
	ds_read_b32 v198, v7 offset:5120
	ds_read_b32 v199, v7 offset:5632
	ds_read_b32 v200, v7 offset:6144
	ds_read_b32 v201, v7 offset:6656
	ds_read_b32 v202, v7 offset:7168
	ds_read_b32 v203, v7 offset:7680
	s_waitcnt lgkmcnt(0)
	v_max_f32_e32 v170, v170, v170
	v_max_f32_e32 v171, v171, v171
	v_max_f32_e32 v172, v172, v172
	v_max_f32_e32 v173, v173, v173
	v_max_f32_e32 v174, v174, v174
	v_max_f32_e32 v175, v175, v175
	v_max_f32_e32 v176, v176, v176
	v_max_f32_e32 v177, v177, v177
	v_max_f32_e32 v196, v196, v196
	v_max_f32_e32 v197, v197, v197
	v_max_f32_e32 v198, v198, v198
	v_max_f32_e32 v199, v199, v199
	v_max_f32_e32 v200, v200, v200
	v_max_f32_e32 v201, v201, v201
	v_max_f32_e32 v202, v202, v202
	v_max_f32_e32 v203, v203, v203
	v_med3_f32 v170, v170, s20, v13
	v_med3_f32 v171, v171, s20, v13
	v_med3_f32 v172, v172, s20, v13
	v_med3_f32 v173, v173, s20, v13
	v_med3_f32 v174, v174, s20, v13
	v_med3_f32 v175, v175, s20, v13
	v_med3_f32 v176, v176, s20, v13
	v_med3_f32 v177, v177, s20, v13
	v_med3_f32 v196, v196, s20, v13
	v_med3_f32 v197, v197, s20, v13
	v_med3_f32 v198, v198, s20, v13
	v_med3_f32 v199, v199, s20, v13
	v_med3_f32 v200, v200, s20, v13
	v_med3_f32 v201, v201, s20, v13
	v_med3_f32 v202, v202, s20, v13
	v_med3_f32 v203, v203, s20, v13
	v_mov_b32_e32 v208, 0
	v_mov_b32_e32 v209, 0
	v_mov_b32_e32 v210, 0
	v_mov_b32_e32 v211, 0
	v_cvt_pk_fp8_f32 v208, v170, v171
	v_cvt_pk_fp8_f32 v209, v174, v175
	v_cvt_pk_fp8_f32 v210, v196, v197
	v_cvt_pk_fp8_f32 v211, v200, v201
	v_cvt_pk_fp8_f32 v208, v172, v173 op_sel:[0,0,1]
	v_cvt_pk_fp8_f32 v209, v176, v177 op_sel:[0,0,1]
	v_cvt_pk_fp8_f32 v210, v198, v199 op_sel:[0,0,1]
	v_cvt_pk_fp8_f32 v211, v202, v203 op_sel:[0,0,1]
	s_nop 0
	global_store_dwordx4 v11, v[208:211], s[14:15]
	ds_read_b32 v170, v9
	ds_read_b32 v171, v9 offset:512
	ds_read_b32 v172, v9 offset:1024
	ds_read_b32 v173, v9 offset:1536
	ds_read_b32 v174, v9 offset:2048
	ds_read_b32 v175, v9 offset:2560
	ds_read_b32 v176, v9 offset:3072
	ds_read_b32 v177, v9 offset:3584
	ds_read_b32 v196, v9 offset:4096
	ds_read_b32 v197, v9 offset:4608
	ds_read_b32 v198, v9 offset:5120
	ds_read_b32 v199, v9 offset:5632
	ds_read_b32 v200, v9 offset:6144
	ds_read_b32 v201, v9 offset:6656
	ds_read_b32 v202, v9 offset:7168
	ds_read_b32 v203, v9 offset:7680
	s_waitcnt lgkmcnt(0)
	v_max_f32_e32 v170, v170, v170
	v_max_f32_e32 v171, v171, v171
	v_max_f32_e32 v172, v172, v172
	v_max_f32_e32 v173, v173, v173
	v_max_f32_e32 v174, v174, v174
	v_max_f32_e32 v175, v175, v175
	v_max_f32_e32 v176, v176, v176
	v_max_f32_e32 v177, v177, v177
	v_max_f32_e32 v196, v196, v196
	v_max_f32_e32 v197, v197, v197
	v_max_f32_e32 v198, v198, v198
	v_max_f32_e32 v199, v199, v199
	v_max_f32_e32 v200, v200, v200
	v_max_f32_e32 v201, v201, v201
	v_max_f32_e32 v202, v202, v202
	v_max_f32_e32 v203, v203, v203
	v_med3_f32 v170, v170, s20, v13
	v_med3_f32 v171, v171, s20, v13
	v_med3_f32 v172, v172, s20, v13
	v_med3_f32 v173, v173, s20, v13
	v_med3_f32 v174, v174, s20, v13
	v_med3_f32 v175, v175, s20, v13
	v_med3_f32 v176, v176, s20, v13
	v_med3_f32 v177, v177, s20, v13
	v_med3_f32 v196, v196, s20, v13
	v_med3_f32 v197, v197, s20, v13
	v_med3_f32 v198, v198, s20, v13
	v_med3_f32 v199, v199, s20, v13
	v_med3_f32 v200, v200, s20, v13
	v_med3_f32 v201, v201, s20, v13
	v_med3_f32 v202, v202, s20, v13
	v_med3_f32 v203, v203, s20, v13
	v_mov_b32_e32 v208, 0
	v_mov_b32_e32 v209, 0
	v_mov_b32_e32 v210, 0
	v_mov_b32_e32 v211, 0
	v_cvt_pk_fp8_f32 v208, v170, v171
	v_cvt_pk_fp8_f32 v209, v174, v175
	v_cvt_pk_fp8_f32 v210, v196, v197
	v_cvt_pk_fp8_f32 v211, v200, v201
	v_cvt_pk_fp8_f32 v208, v172, v173 op_sel:[0,0,1]
	v_cvt_pk_fp8_f32 v209, v176, v177 op_sel:[0,0,1]
	v_cvt_pk_fp8_f32 v210, v198, v199 op_sel:[0,0,1]
	v_cvt_pk_fp8_f32 v211, v202, v203 op_sel:[0,0,1]
	s_nop 0
	global_store_dwordx4 v12, v[208:211], s[14:15]
	s_waitcnt vmcnt(32)
	v_mul_f32_e32 v36, 0x43000000, v36
	v_mul_f32_e32 v37, 0x43000000, v37
	v_mul_f32_e32 v38, 0x43000000, v38
	v_mul_f32_e32 v39, 0x43000000, v39
	ds_write_b128 v4, v[36:39]
	v_mul_f32_e32 v40, 0x43000000, v40
	v_mul_f32_e32 v41, 0x43000000, v41
	v_mul_f32_e32 v42, 0x43000000, v42
	v_mul_f32_e32 v43, 0x43000000, v43
	ds_write_b128 v4, v[40:43] offset:1024
	v_mul_f32_e32 v44, 0x43000000, v44
	v_mul_f32_e32 v45, 0x43000000, v45
	v_mul_f32_e32 v46, 0x43000000, v46
	v_mul_f32_e32 v47, 0x43000000, v47
	ds_write_b128 v4, v[44:47] offset:2048
	v_mul_f32_e32 v48, 0x43000000, v48
	v_mul_f32_e32 v49, 0x43000000, v49
	v_mul_f32_e32 v50, 0x43000000, v50
	v_mul_f32_e32 v51, 0x43000000, v51
	ds_write_b128 v4, v[48:51] offset:3072
	v_mul_f32_e32 v52, 0x43000000, v52
	v_mul_f32_e32 v53, 0x43000000, v53
	v_mul_f32_e32 v54, 0x43000000, v54
	v_mul_f32_e32 v55, 0x43000000, v55
	ds_write_b128 v4, v[52:55] offset:4096
	v_mul_f32_e32 v56, 0x43000000, v56
	v_mul_f32_e32 v57, 0x43000000, v57
	v_mul_f32_e32 v58, 0x43000000, v58
	v_mul_f32_e32 v59, 0x43000000, v59
	ds_write_b128 v4, v[56:59] offset:5120
	v_mul_f32_e32 v60, 0x43000000, v60
	v_mul_f32_e32 v61, 0x43000000, v61
	v_mul_f32_e32 v62, 0x43000000, v62
	v_mul_f32_e32 v63, 0x43000000, v63
	ds_write_b128 v4, v[60:63] offset:6144
	v_mul_f32_e32 v64, 0x43000000, v64
	v_mul_f32_e32 v65, 0x43000000, v65
	v_mul_f32_e32 v66, 0x43000000, v66
	v_mul_f32_e32 v67, 0x43000000, v67
	ds_write_b128 v4, v[64:67] offset:7168
	s_waitcnt lgkmcnt(0)
	s_barrier
; #define GAS __attribute__((address_space(1)))
; #define LAS __attribute__((address_space(3)))
; #define LDS_WAIT() asm volatile("s_waitcnt lgkmcnt(0)" ::: "memory")
;     const int pr = item >> 1, kb = 2 * (pr / nblk) + (item & 1), nb = pr % nblk, k0 = 64 * kb, n0 = 32 * nb;
;     const int nr = n0 + (lane & 31); const int sc = MAP == 1 ? src_col_in(nr) : nr;
;     float v[32];
; #pragma unroll
;     for (int i = 0; i < 32; ++i) v[i] = sc >= 0 ? W[(size_t)(k0 + 2 * i + (lane >> 5)) * Nsrc + sc] : 0.f;
; #pragma unroll
;     for (int i = 0; i < 32; ++i) { const int k = k0 + 2 * i + (lane >> 5); float x = v[i] * wscale; if (KS) x *= (k < ksplit ? ksA[k] : ksB[k - ksplit]); scr[(2 * i + (lane >> 5)) * 33 + (lane & 31)] = x; }
;     LDS_WAIT(); asm volatile("" ::: "memory");
;     const int c = lane & 7;
; #pragma unroll
;     for (int j = 0; j < 4; ++j) { const int n = (lane >> 3) + 8 * j; const LAS float* s = scr + (8 * c) * 33 + n;
;         const unsigned long long o = (unsigned long long)pg8::pk4_fp8(s[0 * 33], s[1 * 33], s[2 * 33], s[3 * 33]) | ((unsigned long long)pg8::pk4_fp8(s[4 * 33], s[5 * 33], s[6 * 33], s[7 * 33]) << 32);
;         *(GAS unsigned long long*)(WT + (size_t)(n0 + n) * K + k0 + 8 * c) = o; }
;     LDS_WAIT(); asm volatile("" ::: "memory");
; __global__ void __launch_bounds__(NWAVES * 64, 2) hybrid_fwd(Args args) {
;     ...
;             if (r < I_O) { if (l >= WO_F8_FROM) p0_transpose_item_f8<true>(args.in[13] + (size_t)l * DM * DM, DM, DM, DM / 32, (unsigned char*)(ws + WS_WO + l * SZ_WO), 64.f, args.in[6] + l * 2048, args.in[12] + l * 2048, 2048, scr, r, lane);
;                 else p0_transpose_item<0, true>(args.in[13] + (size_t)l * DM * DM, DM, DM, DM / 32, (bf16*)(ws + WS_WO + l * SZ_WO), args.in[6] + l * 2048, args.in[12] + l * 2048, 2048, scr, r, lane); continue; } r -= I_O;
;             if (r < I_UP) { p0_transpose_item_f8<true>(args.in[15] + (size_t)l * DM * FF, DM, FF, FF / 32, (unsigned char*)(ws + WS_WUP + l * SZ_WUP), WUP8_SCALE, args.in[14] + l * DM, args.in[14] + l * DM, DM, scr, r, lane); continue; } r -= I_UP;
;             p0_transpose_item_f8<false>(args.in[16] + (size_t)l * FF * DM, FF, DM, DM / 32, (unsigned char*)(ws + WS_WDN + l * SZ_WDN), 128.f, args.in[16], args.in[16], 0, scr, r, lane);
	s_add_i32 s19, s39, 3
	s_min_u32 s19, s19, 31
	s_lshl_b32 s19, s19, 9
	s_add_u32 s12, s22, s19
	s_addc_u32 s13, s23, 0
	global_load_dwordx4 v[36:39], v10, s[12:13]
	s_add_u32 s12, s12, 0x8000
	s_addc_u32 s13, s13, 0
	global_load_dwordx4 v[40:43], v10, s[12:13]
	s_add_u32 s12, s12, 0x8000
	s_addc_u32 s13, s13, 0
	global_load_dwordx4 v[44:47], v10, s[12:13]
	s_add_u32 s12, s12, 0x8000
	s_addc_u32 s13, s13, 0
	global_load_dwordx4 v[48:51], v10, s[12:13]
	s_add_u32 s12, s12, 0x8000
	s_addc_u32 s13, s13, 0
	global_load_dwordx4 v[52:55], v10, s[12:13]
	s_add_u32 s12, s12, 0x8000
	s_addc_u32 s13, s13, 0
	global_load_dwordx4 v[56:59], v10, s[12:13]
	s_add_u32 s12, s12, 0x8000
	s_addc_u32 s13, s13, 0
	global_load_dwordx4 v[60:63], v10, s[12:13]
	s_add_u32 s12, s12, 0x8000
	s_addc_u32 s13, s13, 0
	global_load_dwordx4 v[64:67], v10, s[12:13]
	s_add_i32 s17, s16, 3840
	s_min_u32 s17, s17, 0xfff
	s_lshr_b32 s18, s17, 5
	s_add_i32 s18, s18, 0
	s_and_b32 s19, s17, 31
	s_lshl_b32 s19, s19, 21
	s_lshl_b32 s18, s18, 7
	s_add_u32 s18, s18, s19
	s_add_u32 s14, s4, s18
	s_addc_u32 s15, s5, 0
	ds_read_b32 v170, v6
	ds_read_b32 v171, v6 offset:512
	ds_read_b32 v172, v6 offset:1024
	ds_read_b32 v173, v6 offset:1536
	ds_read_b32 v174, v6 offset:2048
	ds_read_b32 v175, v6 offset:2560
	ds_read_b32 v176, v6 offset:3072
	ds_read_b32 v177, v6 offset:3584
	ds_read_b32 v196, v6 offset:4096
	ds_read_b32 v197, v6 offset:4608
	ds_read_b32 v198, v6 offset:5120
	ds_read_b32 v199, v6 offset:5632
	ds_read_b32 v200, v6 offset:6144
	ds_read_b32 v201, v6 offset:6656
	ds_read_b32 v202, v6 offset:7168
	ds_read_b32 v203, v6 offset:7680
	s_waitcnt lgkmcnt(0)
	v_max_f32_e32 v170, v170, v170
	v_max_f32_e32 v171, v171, v171
	v_max_f32_e32 v172, v172, v172
	v_max_f32_e32 v173, v173, v173
	v_max_f32_e32 v174, v174, v174
	v_max_f32_e32 v175, v175, v175
	v_max_f32_e32 v176, v176, v176
	v_max_f32_e32 v177, v177, v177
	v_max_f32_e32 v196, v196, v196
	v_max_f32_e32 v197, v197, v197
	v_max_f32_e32 v198, v198, v198
	v_max_f32_e32 v199, v199, v199
	v_max_f32_e32 v200, v200, v200
	v_max_f32_e32 v201, v201, v201
	v_max_f32_e32 v202, v202, v202
	v_max_f32_e32 v203, v203, v203
	v_med3_f32 v170, v170, s20, v13
	v_med3_f32 v171, v171, s20, v13
	v_med3_f32 v172, v172, s20, v13
	v_med3_f32 v173, v173, s20, v13
	v_med3_f32 v174, v174, s20, v13
	v_med3_f32 v175, v175, s20, v13
	v_med3_f32 v176, v176, s20, v13
	v_med3_f32 v177, v177, s20, v13
	v_med3_f32 v196, v196, s20, v13
	v_med3_f32 v197, v197, s20, v13
	v_med3_f32 v198, v198, s20, v13
	v_med3_f32 v199, v199, s20, v13
	v_med3_f32 v200, v200, s20, v13
	v_med3_f32 v201, v201, s20, v13
	v_med3_f32 v202, v202, s20, v13
	v_med3_f32 v203, v203, s20, v13
	v_mov_b32_e32 v208, 0
	v_mov_b32_e32 v209, 0
	v_mov_b32_e32 v210, 0
	v_mov_b32_e32 v211, 0
	v_cvt_pk_fp8_f32 v208, v170, v171
	v_cvt_pk_fp8_f32 v209, v174, v175
	v_cvt_pk_fp8_f32 v210, v196, v197
	v_cvt_pk_fp8_f32 v211, v200, v201
	v_cvt_pk_fp8_f32 v208, v172, v173 op_sel:[0,0,1]
	v_cvt_pk_fp8_f32 v209, v176, v177 op_sel:[0,0,1]
	v_cvt_pk_fp8_f32 v210, v198, v199 op_sel:[0,0,1]
	v_cvt_pk_fp8_f32 v211, v202, v203 op_sel:[0,0,1]
	s_nop 0
	global_store_dwordx4 v11, v[208:211], s[14:15]
	ds_read_b32 v170, v8
	ds_read_b32 v171, v8 offset:512
	ds_read_b32 v172, v8 offset:1024
	ds_read_b32 v173, v8 offset:1536
	ds_read_b32 v174, v8 offset:2048
	ds_read_b32 v175, v8 offset:2560
	ds_read_b32 v176, v8 offset:3072
	ds_read_b32 v177, v8 offset:3584
	ds_read_b32 v196, v8 offset:4096
	ds_read_b32 v197, v8 offset:4608
	ds_read_b32 v198, v8 offset:5120
	ds_read_b32 v199, v8 offset:5632
	ds_read_b32 v200, v8 offset:6144
	ds_read_b32 v201, v8 offset:6656
	ds_read_b32 v202, v8 offset:7168
	ds_read_b32 v203, v8 offset:7680
	s_waitcnt lgkmcnt(0)
	v_max_f32_e32 v170, v170, v170
	v_max_f32_e32 v171, v171, v171
	v_max_f32_e32 v172, v172, v172
	v_max_f32_e32 v173, v173, v173
	v_max_f32_e32 v174, v174, v174
	v_max_f32_e32 v175, v175, v175
	v_max_f32_e32 v176, v176, v176
	v_max_f32_e32 v177, v177, v177
	v_max_f32_e32 v196, v196, v196
	v_max_f32_e32 v197, v197, v197
	v_max_f32_e32 v198, v198, v198
	v_max_f32_e32 v199, v199, v199
	v_max_f32_e32 v200, v200, v200
	v_max_f32_e32 v201, v201, v201
	v_max_f32_e32 v202, v202, v202
	v_max_f32_e32 v203, v203, v203
	v_med3_f32 v170, v170, s20, v13
	v_med3_f32 v171, v171, s20, v13
	v_med3_f32 v172, v172, s20, v13
	v_med3_f32 v173, v173, s20, v13
	v_med3_f32 v174, v174, s20, v13
	v_med3_f32 v175, v175, s20, v13
	v_med3_f32 v176, v176, s20, v13
	v_med3_f32 v177, v177, s20, v13
	v_med3_f32 v196, v196, s20, v13
	v_med3_f32 v197, v197, s20, v13
	v_med3_f32 v198, v198, s20, v13
	v_med3_f32 v199, v199, s20, v13
	v_med3_f32 v200, v200, s20, v13
	v_med3_f32 v201, v201, s20, v13
	v_med3_f32 v202, v202, s20, v13
	v_med3_f32 v203, v203, s20, v13
	v_mov_b32_e32 v208, 0
	v_mov_b32_e32 v209, 0
	v_mov_b32_e32 v210, 0
	v_mov_b32_e32 v211, 0
	v_cvt_pk_fp8_f32 v208, v170, v171
	v_cvt_pk_fp8_f32 v209, v174, v175
	v_cvt_pk_fp8_f32 v210, v196, v197
	v_cvt_pk_fp8_f32 v211, v200, v201
	v_cvt_pk_fp8_f32 v208, v172, v173 op_sel:[0,0,1]
	v_cvt_pk_fp8_f32 v209, v176, v177 op_sel:[0,0,1]
	v_cvt_pk_fp8_f32 v210, v198, v199 op_sel:[0,0,1]
	v_cvt_pk_fp8_f32 v211, v202, v203 op_sel:[0,0,1]
	s_nop 0
	global_store_dwordx4 v12, v[208:211], s[14:15]
	s_waitcnt vmcnt(32)
	v_mul_f32_e32 v68, 0x43000000, v68
	v_mul_f32_e32 v69, 0x43000000, v69
	v_mul_f32_e32 v70, 0x43000000, v70
	v_mul_f32_e32 v71, 0x43000000, v71
	ds_write_b128 v5, v[68:71]
	v_mul_f32_e32 v72, 0x43000000, v72
	v_mul_f32_e32 v73, 0x43000000, v73
	v_mul_f32_e32 v74, 0x43000000, v74
	v_mul_f32_e32 v75, 0x43000000, v75
	ds_write_b128 v5, v[72:75] offset:1024
	v_mul_f32_e32 v76, 0x43000000, v76
	v_mul_f32_e32 v77, 0x43000000, v77
	v_mul_f32_e32 v78, 0x43000000, v78
	v_mul_f32_e32 v79, 0x43000000, v79
	ds_write_b128 v5, v[76:79] offset:2048
	v_mul_f32_e32 v80, 0x43000000, v80
	v_mul_f32_e32 v81, 0x43000000, v81
	v_mul_f32_e32 v82, 0x43000000, v82
	v_mul_f32_e32 v83, 0x43000000, v83
	ds_write_b128 v5, v[80:83] offset:3072
	v_mul_f32_e32 v84, 0x43000000, v84
	v_mul_f32_e32 v85, 0x43000000, v85
	v_mul_f32_e32 v86, 0x43000000, v86
	v_mul_f32_e32 v87, 0x43000000, v87
	ds_write_b128 v5, v[84:87] offset:4096
	v_mul_f32_e32 v88, 0x43000000, v88
	v_mul_f32_e32 v89, 0x43000000, v89
	v_mul_f32_e32 v90, 0x43000000, v90
	v_mul_f32_e32 v91, 0x43000000, v91
	ds_write_b128 v5, v[88:91] offset:5120
	v_mul_f32_e32 v92, 0x43000000, v92
	v_mul_f32_e32 v93, 0x43000000, v93
	v_mul_f32_e32 v94, 0x43000000, v94
	v_mul_f32_e32 v95, 0x43000000, v95
	ds_write_b128 v5, v[92:95] offset:6144
	v_mul_f32_e32 v96, 0x43000000, v96
	v_mul_f32_e32 v97, 0x43000000, v97
	v_mul_f32_e32 v98, 0x43000000, v98
	v_mul_f32_e32 v99, 0x43000000, v99
	ds_write_b128 v5, v[96:99] offset:7168
	s_waitcnt lgkmcnt(0)
	s_barrier
; #define GAS __attribute__((address_space(1)))
; #define LAS __attribute__((address_space(3)))
; #define LDS_WAIT() asm volatile("s_waitcnt lgkmcnt(0)" ::: "memory")
;     const int pr = item >> 1, kb = 2 * (pr / nblk) + (item & 1), nb = pr % nblk, k0 = 64 * kb, n0 = 32 * nb;
;     const int nr = n0 + (lane & 31); const int sc = MAP == 1 ? src_col_in(nr) : nr;
;     float v[32];
; #pragma unroll
;     for (int i = 0; i < 32; ++i) v[i] = sc >= 0 ? W[(size_t)(k0 + 2 * i + (lane >> 5)) * Nsrc + sc] : 0.f;
; #pragma unroll
;     for (int i = 0; i < 32; ++i) { const int k = k0 + 2 * i + (lane >> 5); float x = v[i] * wscale; if (KS) x *= (k < ksplit ? ksA[k] : ksB[k - ksplit]); scr[(2 * i + (lane >> 5)) * 33 + (lane & 31)] = x; }
;     LDS_WAIT(); asm volatile("" ::: "memory");
;     const int c = lane & 7;
; #pragma unroll
;     for (int j = 0; j < 4; ++j) { const int n = (lane >> 3) + 8 * j; const LAS float* s = scr + (8 * c) * 33 + n;
;         const unsigned long long o = (unsigned long long)pg8::pk4_fp8(s[0 * 33], s[1 * 33], s[2 * 33], s[3 * 33]) | ((unsigned long long)pg8::pk4_fp8(s[4 * 33], s[5 * 33], s[6 * 33], s[7 * 33]) << 32);
;         *(GAS unsigned long long*)(WT + (size_t)(n0 + n) * K + k0 + 8 * c) = o; }
;     LDS_WAIT(); asm volatile("" ::: "memory");
; __global__ void __launch_bounds__(NWAVES * 64, 2) hybrid_fwd(Args args) {
;     ...
;             if (r < I_O) { if (l >= WO_F8_FROM) p0_transpose_item_f8<true>(args.in[13] + (size_t)l * DM * DM, DM, DM, DM / 32, (unsigned char*)(ws + WS_WO + l * SZ_WO), 64.f, args.in[6] + l * 2048, args.in[12] + l * 2048, 2048, scr, r, lane);
;                 else p0_transpose_item<0, true>(args.in[13] + (size_t)l * DM * DM, DM, DM, DM / 32, (bf16*)(ws + WS_WO + l * SZ_WO), args.in[6] + l * 2048, args.in[12] + l * 2048, 2048, scr, r, lane); continue; } r -= I_O;
;             if (r < I_UP) { p0_transpose_item_f8<true>(args.in[15] + (size_t)l * DM * FF, DM, FF, FF / 32, (unsigned char*)(ws + WS_WUP + l * SZ_WUP), WUP8_SCALE, args.in[14] + l * DM, args.in[14] + l * DM, DM, scr, r, lane); continue; } r -= I_UP;
;             p0_transpose_item_f8<false>(args.in[16] + (size_t)l * FF * DM, FF, DM, DM / 32, (unsigned char*)(ws + WS_WDN + l * SZ_WDN), 128.f, args.in[16], args.in[16], 0, scr, r, lane);
	s_add_i32 s19, s39, 6
	s_min_u32 s19, s19, 31
	s_lshl_b32 s19, s19, 9
	s_add_u32 s12, s22, s19
	s_addc_u32 s13, s23, 0
	global_load_dwordx4 v[68:71], v10, s[12:13]
	s_add_u32 s12, s12, 0x8000
	s_addc_u32 s13, s13, 0
	global_load_dwordx4 v[72:75], v10, s[12:13]
	s_add_u32 s12, s12, 0x8000
	s_addc_u32 s13, s13, 0
	global_load_dwordx4 v[76:79], v10, s[12:13]
	s_add_u32 s12, s12, 0x8000
	s_addc_u32 s13, s13, 0
	global_load_dwordx4 v[80:83], v10, s[12:13]
	s_add_u32 s12, s12, 0x8000
	s_addc_u32 s13, s13, 0
	global_load_dwordx4 v[84:87], v10, s[12:13]
	s_add_u32 s12, s12, 0x8000
	s_addc_u32 s13, s13, 0
	global_load_dwordx4 v[88:91], v10, s[12:13]
	s_add_u32 s12, s12, 0x8000
	s_addc_u32 s13, s13, 0
	global_load_dwordx4 v[92:95], v10, s[12:13]
	s_add_u32 s12, s12, 0x8000
	s_addc_u32 s13, s13, 0
	global_load_dwordx4 v[96:99], v10, s[12:13]
	s_add_i32 s17, s16, 3936
	s_min_u32 s17, s17, 0xfff
	s_lshr_b32 s18, s17, 5
	s_add_i32 s18, s18, 0
	s_and_b32 s19, s17, 31
	s_lshl_b32 s19, s19, 21
	s_lshl_b32 s18, s18, 7
	s_add_u32 s18, s18, s19
	s_add_u32 s14, s4, s18
	s_addc_u32 s15, s5, 0
	ds_read_b32 v170, v7
	ds_read_b32 v171, v7 offset:512
	ds_read_b32 v172, v7 offset:1024
	ds_read_b32 v173, v7 offset:1536
	ds_read_b32 v174, v7 offset:2048
	ds_read_b32 v175, v7 offset:2560
	ds_read_b32 v176, v7 offset:3072
	ds_read_b32 v177, v7 offset:3584
	ds_read_b32 v196, v7 offset:4096
	ds_read_b32 v197, v7 offset:4608
	ds_read_b32 v198, v7 offset:5120
	ds_read_b32 v199, v7 offset:5632
	ds_read_b32 v200, v7 offset:6144
	ds_read_b32 v201, v7 offset:6656
	ds_read_b32 v202, v7 offset:7168
	ds_read_b32 v203, v7 offset:7680
	s_waitcnt lgkmcnt(0)
	v_max_f32_e32 v170, v170, v170
	v_max_f32_e32 v171, v171, v171
	v_max_f32_e32 v172, v172, v172
	v_max_f32_e32 v173, v173, v173
	v_max_f32_e32 v174, v174, v174
	v_max_f32_e32 v175, v175, v175
	v_max_f32_e32 v176, v176, v176
	v_max_f32_e32 v177, v177, v177
	v_max_f32_e32 v196, v196, v196
	v_max_f32_e32 v197, v197, v197
	v_max_f32_e32 v198, v198, v198
	v_max_f32_e32 v199, v199, v199
	v_max_f32_e32 v200, v200, v200
	v_max_f32_e32 v201, v201, v201
	v_max_f32_e32 v202, v202, v202
	v_max_f32_e32 v203, v203, v203
	v_med3_f32 v170, v170, s20, v13
	v_med3_f32 v171, v171, s20, v13
	v_med3_f32 v172, v172, s20, v13
	v_med3_f32 v173, v173, s20, v13
	v_med3_f32 v174, v174, s20, v13
	v_med3_f32 v175, v175, s20, v13
	v_med3_f32 v176, v176, s20, v13
	v_med3_f32 v177, v177, s20, v13
	v_med3_f32 v196, v196, s20, v13
	v_med3_f32 v197, v197, s20, v13
	v_med3_f32 v198, v198, s20, v13
	v_med3_f32 v199, v199, s20, v13
	v_med3_f32 v200, v200, s20, v13
	v_med3_f32 v201, v201, s20, v13
	v_med3_f32 v202, v202, s20, v13
	v_med3_f32 v203, v203, s20, v13
	v_mov_b32_e32 v208, 0
	v_mov_b32_e32 v209, 0
	v_mov_b32_e32 v210, 0
	v_mov_b32_e32 v211, 0
	v_cvt_pk_fp8_f32 v208, v170, v171
	v_cvt_pk_fp8_f32 v209, v174, v175
	v_cvt_pk_fp8_f32 v210, v196, v197
	v_cvt_pk_fp8_f32 v211, v200, v201
	v_cvt_pk_fp8_f32 v208, v172, v173 op_sel:[0,0,1]
	v_cvt_pk_fp8_f32 v209, v176, v177 op_sel:[0,0,1]
	v_cvt_pk_fp8_f32 v210, v198, v199 op_sel:[0,0,1]
	v_cvt_pk_fp8_f32 v211, v202, v203 op_sel:[0,0,1]
	s_nop 0
	global_store_dwordx4 v11, v[208:211], s[14:15]
	ds_read_b32 v170, v9
	ds_read_b32 v171, v9 offset:512
	ds_read_b32 v172, v9 offset:1024
	ds_read_b32 v173, v9 offset:1536
	ds_read_b32 v174, v9 offset:2048
	ds_read_b32 v175, v9 offset:2560
	ds_read_b32 v176, v9 offset:3072
	ds_read_b32 v177, v9 offset:3584
	ds_read_b32 v196, v9 offset:4096
	ds_read_b32 v197, v9 offset:4608
	ds_read_b32 v198, v9 offset:5120
	ds_read_b32 v199, v9 offset:5632
	ds_read_b32 v200, v9 offset:6144
	ds_read_b32 v201, v9 offset:6656
	ds_read_b32 v202, v9 offset:7168
	ds_read_b32 v203, v9 offset:7680
	s_waitcnt lgkmcnt(0)
	v_max_f32_e32 v170, v170, v170
	v_max_f32_e32 v171, v171, v171
	v_max_f32_e32 v172, v172, v172
	v_max_f32_e32 v173, v173, v173
	v_max_f32_e32 v174, v174, v174
	v_max_f32_e32 v175, v175, v175
	v_max_f32_e32 v176, v176, v176
	v_max_f32_e32 v177, v177, v177
	v_max_f32_e32 v196, v196, v196
	v_max_f32_e32 v197, v197, v197
	v_max_f32_e32 v198, v198, v198
	v_max_f32_e32 v199, v199, v199
	v_max_f32_e32 v200, v200, v200
	v_max_f32_e32 v201, v201, v201
	v_max_f32_e32 v202, v202, v202
	v_max_f32_e32 v203, v203, v203
	v_med3_f32 v170, v170, s20, v13
	v_med3_f32 v171, v171, s20, v13
	v_med3_f32 v172, v172, s20, v13
	v_med3_f32 v173, v173, s20, v13
	v_med3_f32 v174, v174, s20, v13
	v_med3_f32 v175, v175, s20, v13
	v_med3_f32 v176, v176, s20, v13
	v_med3_f32 v177, v177, s20, v13
	v_med3_f32 v196, v196, s20, v13
	v_med3_f32 v197, v197, s20, v13
	v_med3_f32 v198, v198, s20, v13
	v_med3_f32 v199, v199, s20, v13
	v_med3_f32 v200, v200, s20, v13
	v_med3_f32 v201, v201, s20, v13
	v_med3_f32 v202, v202, s20, v13
	v_med3_f32 v203, v203, s20, v13
	v_mov_b32_e32 v208, 0
	v_mov_b32_e32 v209, 0
	v_mov_b32_e32 v210, 0
	v_mov_b32_e32 v211, 0
	v_cvt_pk_fp8_f32 v208, v170, v171
	v_cvt_pk_fp8_f32 v209, v174, v175
	v_cvt_pk_fp8_f32 v210, v196, v197
	v_cvt_pk_fp8_f32 v211, v200, v201
	v_cvt_pk_fp8_f32 v208, v172, v173 op_sel:[0,0,1]
	v_cvt_pk_fp8_f32 v209, v176, v177 op_sel:[0,0,1]
	v_cvt_pk_fp8_f32 v210, v198, v199 op_sel:[0,0,1]
	v_cvt_pk_fp8_f32 v211, v202, v203 op_sel:[0,0,1]
	s_nop 0
	global_store_dwordx4 v12, v[208:211], s[14:15]
	s_waitcnt vmcnt(32)
	v_mul_f32_e32 v100, 0x43000000, v100
	v_mul_f32_e32 v101, 0x43000000, v101
	v_mul_f32_e32 v102, 0x43000000, v102
	v_mul_f32_e32 v103, 0x43000000, v103
	ds_write_b128 v4, v[100:103]
	v_mul_f32_e32 v104, 0x43000000, v104
	v_mul_f32_e32 v105, 0x43000000, v105
	v_mul_f32_e32 v106, 0x43000000, v106
	v_mul_f32_e32 v107, 0x43000000, v107
	ds_write_b128 v4, v[104:107] offset:1024
	v_mul_f32_e32 v108, 0x43000000, v108
	v_mul_f32_e32 v109, 0x43000000, v109
	v_mul_f32_e32 v110, 0x43000000, v110
	v_mul_f32_e32 v111, 0x43000000, v111
	ds_write_b128 v4, v[108:111] offset:2048
	v_mul_f32_e32 v112, 0x43000000, v112
	v_mul_f32_e32 v113, 0x43000000, v113
	v_mul_f32_e32 v114, 0x43000000, v114
	v_mul_f32_e32 v115, 0x43000000, v115
	ds_write_b128 v4, v[112:115] offset:3072
	v_mul_f32_e32 v116, 0x43000000, v116
	v_mul_f32_e32 v117, 0x43000000, v117
	v_mul_f32_e32 v118, 0x43000000, v118
	v_mul_f32_e32 v119, 0x43000000, v119
	ds_write_b128 v4, v[116:119] offset:4096
	v_mul_f32_e32 v120, 0x43000000, v120
	v_mul_f32_e32 v121, 0x43000000, v121
	v_mul_f32_e32 v122, 0x43000000, v122
	v_mul_f32_e32 v123, 0x43000000, v123
	ds_write_b128 v4, v[120:123] offset:5120
	v_mul_f32_e32 v124, 0x43000000, v124
	v_mul_f32_e32 v125, 0x43000000, v125
	v_mul_f32_e32 v126, 0x43000000, v126
	v_mul_f32_e32 v127, 0x43000000, v127
	ds_write_b128 v4, v[124:127] offset:6144
	v_mul_f32_e32 v128, 0x43000000, v128
	v_mul_f32_e32 v129, 0x43000000, v129
	v_mul_f32_e32 v130, 0x43000000, v130
	v_mul_f32_e32 v131, 0x43000000, v131
	ds_write_b128 v4, v[128:131] offset:7168
	s_waitcnt lgkmcnt(0)
	s_barrier
; #define GAS __attribute__((address_space(1)))
; #define LAS __attribute__((address_space(3)))
; #define LDS_WAIT() asm volatile("s_waitcnt lgkmcnt(0)" ::: "memory")
;     const int pr = item >> 1, kb = 2 * (pr / nblk) + (item & 1), nb = pr % nblk, k0 = 64 * kb, n0 = 32 * nb;
;     const int nr = n0 + (lane & 31); const int sc = MAP == 1 ? src_col_in(nr) : nr;
;     float v[32];
; #pragma unroll
;     for (int i = 0; i < 32; ++i) v[i] = sc >= 0 ? W[(size_t)(k0 + 2 * i + (lane >> 5)) * Nsrc + sc] : 0.f;
; #pragma unroll
;     for (int i = 0; i < 32; ++i) { const int k = k0 + 2 * i + (lane >> 5); float x = v[i] * wscale; if (KS) x *= (k < ksplit ? ksA[k] : ksB[k - ksplit]); scr[(2 * i + (lane >> 5)) * 33 + (lane & 31)] = x; }
;     LDS_WAIT(); asm volatile("" ::: "memory");
;     const int c = lane & 7;
; #pragma unroll
;     for (int j = 0; j < 4; ++j) { const int n = (lane >> 3) + 8 * j; const LAS float* s = scr + (8 * c) * 33 + n;
;         const unsigned long long o = (unsigned long long)pg8::pk4_fp8(s[0 * 33], s[1 * 33], s[2 * 33], s[3 * 33]) | ((unsigned long long)pg8::pk4_fp8(s[4 * 33], s[5 * 33], s[6 * 33], s[7 * 33]) << 32);
;         *(GAS unsigned long long*)(WT + (size_t)(n0 + n) * K + k0 + 8 * c) = o; }
;     LDS_WAIT(); asm volatile("" ::: "memory");
; __global__ void __launch_bounds__(NWAVES * 64, 2) hybrid_fwd(Args args) {
;     ...
;             if (r < I_O) { if (l >= WO_F8_FROM) p0_transpose_item_f8<true>(args.in[13] + (size_t)l * DM * DM, DM, DM, DM / 32, (unsigned char*)(ws + WS_WO + l * SZ_WO), 64.f, args.in[6] + l * 2048, args.in[12] + l * 2048, 2048, scr, r, lane);
;                 else p0_transpose_item<0, true>(args.in[13] + (size_t)l * DM * DM, DM, DM, DM / 32, (bf16*)(ws + WS_WO + l * SZ_WO), args.in[6] + l * 2048, args.in[12] + l * 2048, 2048, scr, r, lane); continue; } r -= I_O;
;             if (r < I_UP) { p0_transpose_item_f8<true>(args.in[15] + (size_t)l * DM * FF, DM, FF, FF / 32, (unsigned char*)(ws + WS_WUP + l * SZ_WUP), WUP8_SCALE, args.in[14] + l * DM, args.in[14] + l * DM, DM, scr, r, lane); continue; } r -= I_UP;
;             p0_transpose_item_f8<false>(args.in[16] + (size_t)l * FF * DM, FF, DM, DM / 32, (unsigned char*)(ws + WS_WDN + l * SZ_WDN), 128.f, args.in[16], args.in[16], 0, scr, r, lane);
	s_add_i32 s19, s39, 9
	s_min_u32 s19, s19, 31
	s_lshl_b32 s19, s19, 9
	s_add_u32 s12, s22, s19
	s_addc_u32 s13, s23, 0
	global_load_dwordx4 v[100:103], v10, s[12:13]
	s_add_u32 s12, s12, 0x8000
	s_addc_u32 s13, s13, 0
	global_load_dwordx4 v[104:107], v10, s[12:13]
	s_add_u32 s12, s12, 0x8000
	s_addc_u32 s13, s13, 0
	global_load_dwordx4 v[108:111], v10, s[12:13]
	s_add_u32 s12, s12, 0x8000
	s_addc_u32 s13, s13, 0
	global_load_dwordx4 v[112:115], v10, s[12:13]
	s_add_u32 s12, s12, 0x8000
	s_addc_u32 s13, s13, 0
	global_load_dwordx4 v[116:119], v10, s[12:13]
	s_add_u32 s12, s12, 0x8000
	s_addc_u32 s13, s13, 0
	global_load_dwordx4 v[120:123], v10, s[12:13]
	s_add_u32 s12, s12, 0x8000
	s_addc_u32 s13, s13, 0
	global_load_dwordx4 v[124:127], v10, s[12:13]
	s_add_u32 s12, s12, 0x8000
	s_addc_u32 s13, s13, 0
	global_load_dwordx4 v[128:131], v10, s[12:13]
	s_add_i32 s17, s16, 4032
	s_min_u32 s17, s17, 0xfff
	s_lshr_b32 s18, s17, 5
	s_add_i32 s18, s18, 0
	s_and_b32 s19, s17, 31
	s_lshl_b32 s19, s19, 21
	s_lshl_b32 s18, s18, 7
	s_add_u32 s18, s18, s19
	s_add_u32 s14, s4, s18
	s_addc_u32 s15, s5, 0
	ds_read_b32 v170, v6
	ds_read_b32 v171, v6 offset:512
	ds_read_b32 v172, v6 offset:1024
	ds_read_b32 v173, v6 offset:1536
	ds_read_b32 v174, v6 offset:2048
	ds_read_b32 v175, v6 offset:2560
	ds_read_b32 v176, v6 offset:3072
	ds_read_b32 v177, v6 offset:3584
	ds_read_b32 v196, v6 offset:4096
	ds_read_b32 v197, v6 offset:4608
	ds_read_b32 v198, v6 offset:5120
	ds_read_b32 v199, v6 offset:5632
	ds_read_b32 v200, v6 offset:6144
	ds_read_b32 v201, v6 offset:6656
	ds_read_b32 v202, v6 offset:7168
	ds_read_b32 v203, v6 offset:7680
	s_waitcnt lgkmcnt(0)
	v_max_f32_e32 v170, v170, v170
	v_max_f32_e32 v171, v171, v171
	v_max_f32_e32 v172, v172, v172
	v_max_f32_e32 v173, v173, v173
	v_max_f32_e32 v174, v174, v174
	v_max_f32_e32 v175, v175, v175
	v_max_f32_e32 v176, v176, v176
	v_max_f32_e32 v177, v177, v177
	v_max_f32_e32 v196, v196, v196
	v_max_f32_e32 v197, v197, v197
	v_max_f32_e32 v198, v198, v198
	v_max_f32_e32 v199, v199, v199
	v_max_f32_e32 v200, v200, v200
	v_max_f32_e32 v201, v201, v201
	v_max_f32_e32 v202, v202, v202
	v_max_f32_e32 v203, v203, v203
	v_med3_f32 v170, v170, s20, v13
	v_med3_f32 v171, v171, s20, v13
	v_med3_f32 v172, v172, s20, v13
	v_med3_f32 v173, v173, s20, v13
	v_med3_f32 v174, v174, s20, v13
	v_med3_f32 v175, v175, s20, v13
	v_med3_f32 v176, v176, s20, v13
	v_med3_f32 v177, v177, s20, v13
	v_med3_f32 v196, v196, s20, v13
	v_med3_f32 v197, v197, s20, v13
	v_med3_f32 v198, v198, s20, v13
	v_med3_f32 v199, v199, s20, v13
	v_med3_f32 v200, v200, s20, v13
	v_med3_f32 v201, v201, s20, v13
	v_med3_f32 v202, v202, s20, v13
	v_med3_f32 v203, v203, s20, v13
	v_mov_b32_e32 v208, 0
	v_mov_b32_e32 v209, 0
	v_mov_b32_e32 v210, 0
	v_mov_b32_e32 v211, 0
	v_cvt_pk_fp8_f32 v208, v170, v171
	v_cvt_pk_fp8_f32 v209, v174, v175
	v_cvt_pk_fp8_f32 v210, v196, v197
	v_cvt_pk_fp8_f32 v211, v200, v201
	v_cvt_pk_fp8_f32 v208, v172, v173 op_sel:[0,0,1]
	v_cvt_pk_fp8_f32 v209, v176, v177 op_sel:[0,0,1]
	v_cvt_pk_fp8_f32 v210, v198, v199 op_sel:[0,0,1]
	v_cvt_pk_fp8_f32 v211, v202, v203 op_sel:[0,0,1]
	s_nop 0
	global_store_dwordx4 v11, v[208:211], s[14:15]
	ds_read_b32 v170, v8
	ds_read_b32 v171, v8 offset:512
	ds_read_b32 v172, v8 offset:1024
	ds_read_b32 v173, v8 offset:1536
	ds_read_b32 v174, v8 offset:2048
	ds_read_b32 v175, v8 offset:2560
	ds_read_b32 v176, v8 offset:3072
	ds_read_b32 v177, v8 offset:3584
	ds_read_b32 v196, v8 offset:4096
	ds_read_b32 v197, v8 offset:4608
	ds_read_b32 v198, v8 offset:5120
	ds_read_b32 v199, v8 offset:5632
	ds_read_b32 v200, v8 offset:6144
	ds_read_b32 v201, v8 offset:6656
	ds_read_b32 v202, v8 offset:7168
	ds_read_b32 v203, v8 offset:7680
	s_waitcnt lgkmcnt(0)
	v_max_f32_e32 v170, v170, v170
	v_max_f32_e32 v171, v171, v171
	v_max_f32_e32 v172, v172, v172
	v_max_f32_e32 v173, v173, v173
	v_max_f32_e32 v174, v174, v174
	v_max_f32_e32 v175, v175, v175
	v_max_f32_e32 v176, v176, v176
	v_max_f32_e32 v177, v177, v177
	v_max_f32_e32 v196, v196, v196
	v_max_f32_e32 v197, v197, v197
	v_max_f32_e32 v198, v198, v198
	v_max_f32_e32 v199, v199, v199
	v_max_f32_e32 v200, v200, v200
	v_max_f32_e32 v201, v201, v201
	v_max_f32_e32 v202, v202, v202
	v_max_f32_e32 v203, v203, v203
	v_med3_f32 v170, v170, s20, v13
	v_med3_f32 v171, v171, s20, v13
	v_med3_f32 v172, v172, s20, v13
	v_med3_f32 v173, v173, s20, v13
	v_med3_f32 v174, v174, s20, v13
	v_med3_f32 v175, v175, s20, v13
	v_med3_f32 v176, v176, s20, v13
	v_med3_f32 v177, v177, s20, v13
	v_med3_f32 v196, v196, s20, v13
	v_med3_f32 v197, v197, s20, v13
	v_med3_f32 v198, v198, s20, v13
	v_med3_f32 v199, v199, s20, v13
	v_med3_f32 v200, v200, s20, v13
	v_med3_f32 v201, v201, s20, v13
	v_med3_f32 v202, v202, s20, v13
	v_med3_f32 v203, v203, s20, v13
	v_mov_b32_e32 v208, 0
	v_mov_b32_e32 v209, 0
	v_mov_b32_e32 v210, 0
	v_mov_b32_e32 v211, 0
	v_cvt_pk_fp8_f32 v208, v170, v171
	v_cvt_pk_fp8_f32 v209, v174, v175
	v_cvt_pk_fp8_f32 v210, v196, v197
	v_cvt_pk_fp8_f32 v211, v200, v201
	v_cvt_pk_fp8_f32 v208, v172, v173 op_sel:[0,0,1]
	v_cvt_pk_fp8_f32 v209, v176, v177 op_sel:[0,0,1]
	v_cvt_pk_fp8_f32 v210, v198, v199 op_sel:[0,0,1]
	v_cvt_pk_fp8_f32 v211, v202, v203 op_sel:[0,0,1]
	s_nop 0
	global_store_dwordx4 v12, v[208:211], s[14:15]
	s_waitcnt vmcnt(32)
	v_mul_f32_e32 v132, v20, v132
	v_mul_f32_e32 v133, v20, v133
	v_mul_f32_e32 v134, v20, v134
	v_mul_f32_e32 v135, v20, v135
	ds_write_b128 v5, v[132:135]
	v_mul_f32_e32 v136, v21, v136
	v_mul_f32_e32 v137, v21, v137
	v_mul_f32_e32 v138, v21, v138
	v_mul_f32_e32 v139, v21, v139
	ds_write_b128 v5, v[136:139] offset:1024
	v_mul_f32_e32 v140, v22, v140
	v_mul_f32_e32 v141, v22, v141
	v_mul_f32_e32 v142, v22, v142
	v_mul_f32_e32 v143, v22, v143
	ds_write_b128 v5, v[140:143] offset:2048
	v_mul_f32_e32 v144, v23, v144
	v_mul_f32_e32 v145, v23, v145
	v_mul_f32_e32 v146, v23, v146
	v_mul_f32_e32 v147, v23, v147
	ds_write_b128 v5, v[144:147] offset:3072
	v_mul_f32_e32 v148, v24, v148
	v_mul_f32_e32 v149, v24, v149
	v_mul_f32_e32 v150, v24, v150
	v_mul_f32_e32 v151, v24, v151
	ds_write_b128 v5, v[148:151] offset:4096
	v_mul_f32_e32 v152, v25, v152
	v_mul_f32_e32 v153, v25, v153
	v_mul_f32_e32 v154, v25, v154
	v_mul_f32_e32 v155, v25, v155
	ds_write_b128 v5, v[152:155] offset:5120
	v_mul_f32_e32 v156, v26, v156
	v_mul_f32_e32 v157, v26, v157
	v_mul_f32_e32 v158, v26, v158
	v_mul_f32_e32 v159, v26, v159
	ds_write_b128 v5, v[156:159] offset:6144
	v_mul_f32_e32 v160, v27, v160
	v_mul_f32_e32 v161, v27, v161
	v_mul_f32_e32 v162, v27, v162
	v_mul_f32_e32 v163, v27, v163
	ds_write_b128 v5, v[160:163] offset:7168
	s_waitcnt lgkmcnt(0)
	s_barrier
; #define GAS __attribute__((address_space(1)))
; #define LAS __attribute__((address_space(3)))
; #define LDS_WAIT() asm volatile("s_waitcnt lgkmcnt(0)" ::: "memory")
;     const int pr = item >> 1, kb = 2 * (pr / nblk) + (item & 1), nb = pr % nblk, k0 = 64 * kb, n0 = 32 * nb;
;     const int nr = n0 + (lane & 31); const int sc = MAP == 1 ? src_col_in(nr) : nr;
;     float v[32];
; #pragma unroll
;     for (int i = 0; i < 32; ++i) v[i] = sc >= 0 ? W[(size_t)(k0 + 2 * i + (lane >> 5)) * Nsrc + sc] : 0.f;
; #pragma unroll
;     for (int i = 0; i < 32; ++i) { const int k = k0 + 2 * i + (lane >> 5); float x = v[i] * wscale; if (KS) x *= (k < ksplit ? ksA[k] : ksB[k - ksplit]); scr[(2 * i + (lane >> 5)) * 33 + (lane & 31)] = x; }
;     LDS_WAIT(); asm volatile("" ::: "memory");
;     const int c = lane & 7;
; #pragma unroll
;     for (int j = 0; j < 4; ++j) { const int n = (lane >> 3) + 8 * j; const LAS float* s = scr + (8 * c) * 33 + n;
;         const unsigned long long o = (unsigned long long)pg8::pk4_fp8(s[0 * 33], s[1 * 33], s[2 * 33], s[3 * 33]) | ((unsigned long long)pg8::pk4_fp8(s[4 * 33], s[5 * 33], s[6 * 33], s[7 * 33]) << 32);
;         *(GAS unsigned long long*)(WT + (size_t)(n0 + n) * K + k0 + 8 * c) = o; }
;     LDS_WAIT(); asm volatile("" ::: "memory");
; __global__ void __launch_bounds__(NWAVES * 64, 2) hybrid_fwd(Args args) {
;     ...
;             if (r < I_O) { if (l >= WO_F8_FROM) p0_transpose_item_f8<true>(args.in[13] + (size_t)l * DM * DM, DM, DM, DM / 32, (unsigned char*)(ws + WS_WO + l * SZ_WO), 64.f, args.in[6] + l * 2048, args.in[12] + l * 2048, 2048, scr, r, lane);
;                 else p0_transpose_item<0, true>(args.in[13] + (size_t)l * DM * DM, DM, DM, DM / 32, (bf16*)(ws + WS_WO + l * SZ_WO), args.in[6] + l * 2048, args.in[12] + l * 2048, 2048, scr, r, lane); continue; } r -= I_O;
;             if (r < I_UP) { p0_transpose_item_f8<true>(args.in[15] + (size_t)l * DM * FF, DM, FF, FF / 32, (unsigned char*)(ws + WS_WUP + l * SZ_WUP), WUP8_SCALE, args.in[14] + l * DM, args.in[14] + l * DM, DM, scr, r, lane); continue; } r -= I_UP;
;             p0_transpose_item_f8<false>(args.in[16] + (size_t)l * FF * DM, FF, DM, DM / 32, (unsigned char*)(ws + WS_WDN + l * SZ_WDN), 128.f, args.in[16], args.in[16], 0, scr, r, lane);
	s_add_i32 s19, s39, 12
	s_min_u32 s19, s19, 31
	s_lshl_b32 s19, s19, 9
	s_add_u32 s12, s22, s19
	s_addc_u32 s13, s23, 0
	global_load_dwordx4 v[132:135], v10, s[12:13]
	s_add_u32 s12, s12, 0x8000
	s_addc_u32 s13, s13, 0
	global_load_dwordx4 v[136:139], v10, s[12:13]
	s_add_u32 s12, s12, 0x8000
	s_addc_u32 s13, s13, 0
	global_load_dwordx4 v[140:143], v10, s[12:13]
	s_add_u32 s12, s12, 0x8000
	s_addc_u32 s13, s13, 0
	global_load_dwordx4 v[144:147], v10, s[12:13]
	s_add_u32 s12, s12, 0x8000
	s_addc_u32 s13, s13, 0
	global_load_dwordx4 v[148:151], v10, s[12:13]
	s_add_u32 s12, s12, 0x8000
	s_addc_u32 s13, s13, 0
	global_load_dwordx4 v[152:155], v10, s[12:13]
	s_add_u32 s12, s12, 0x8000
	s_addc_u32 s13, s13, 0
	global_load_dwordx4 v[156:159], v10, s[12:13]
	s_add_u32 s12, s12, 0x8000
	s_addc_u32 s13, s13, 0
	global_load_dwordx4 v[160:163], v10, s[12:13]
	s_add_i32 s19, s39, 0
	s_min_u32 s19, s19, 31
	s_lshl_b32 s19, s19, 19
	s_add_u32 s14, s50, s19
	s_addc_u32 s15, s51, 0
	ds_read_b32 v170, v7
	ds_read_b32 v171, v7 offset:512
	ds_read_b32 v172, v7 offset:1024
	ds_read_b32 v173, v7 offset:1536
	ds_read_b32 v174, v7 offset:2048
	ds_read_b32 v175, v7 offset:2560
	ds_read_b32 v176, v7 offset:3072
	ds_read_b32 v177, v7 offset:3584
	ds_read_b32 v196, v7 offset:4096
	ds_read_b32 v197, v7 offset:4608
	ds_read_b32 v198, v7 offset:5120
	ds_read_b32 v199, v7 offset:5632
	ds_read_b32 v200, v7 offset:6144
	ds_read_b32 v201, v7 offset:6656
	ds_read_b32 v202, v7 offset:7168
	ds_read_b32 v203, v7 offset:7680
	s_waitcnt lgkmcnt(0)
	v_max_f32_e32 v170, v170, v170
	v_max_f32_e32 v171, v171, v171
	v_max_f32_e32 v172, v172, v172
	v_max_f32_e32 v173, v173, v173
	v_max_f32_e32 v174, v174, v174
	v_max_f32_e32 v175, v175, v175
	v_max_f32_e32 v176, v176, v176
	v_max_f32_e32 v177, v177, v177
	v_max_f32_e32 v196, v196, v196
	v_max_f32_e32 v197, v197, v197
	v_max_f32_e32 v198, v198, v198
	v_max_f32_e32 v199, v199, v199
	v_max_f32_e32 v200, v200, v200
	v_max_f32_e32 v201, v201, v201
	v_max_f32_e32 v202, v202, v202
	v_max_f32_e32 v203, v203, v203
	v_med3_f32 v170, v170, s20, v13
	v_med3_f32 v171, v171, s20, v13
	v_med3_f32 v172, v172, s20, v13
	v_med3_f32 v173, v173, s20, v13
	v_med3_f32 v174, v174, s20, v13
	v_med3_f32 v175, v175, s20, v13
	v_med3_f32 v176, v176, s20, v13
	v_med3_f32 v177, v177, s20, v13
	v_med3_f32 v196, v196, s20, v13
	v_med3_f32 v197, v197, s20, v13
	v_med3_f32 v198, v198, s20, v13
	v_med3_f32 v199, v199, s20, v13
	v_med3_f32 v200, v200, s20, v13
	v_med3_f32 v201, v201, s20, v13
	v_med3_f32 v202, v202, s20, v13
	v_med3_f32 v203, v203, s20, v13
	v_mov_b32_e32 v208, 0
	v_mov_b32_e32 v209, 0
	v_mov_b32_e32 v210, 0
	v_mov_b32_e32 v211, 0
	v_cvt_pk_fp8_f32 v208, v170, v171
	v_cvt_pk_fp8_f32 v209, v174, v175
	v_cvt_pk_fp8_f32 v210, v196, v197
	v_cvt_pk_fp8_f32 v211, v200, v201
	v_cvt_pk_fp8_f32 v208, v172, v173 op_sel:[0,0,1]
	v_cvt_pk_fp8_f32 v209, v176, v177 op_sel:[0,0,1]
	v_cvt_pk_fp8_f32 v210, v198, v199 op_sel:[0,0,1]
	v_cvt_pk_fp8_f32 v211, v202, v203 op_sel:[0,0,1]
	s_nop 0
	global_store_dwordx4 v28, v[208:211], s[14:15]
	ds_read_b32 v170, v9
	ds_read_b32 v171, v9 offset:512
	ds_read_b32 v172, v9 offset:1024
	ds_read_b32 v173, v9 offset:1536
	ds_read_b32 v174, v9 offset:2048
	ds_read_b32 v175, v9 offset:2560
	ds_read_b32 v176, v9 offset:3072
	ds_read_b32 v177, v9 offset:3584
	ds_read_b32 v196, v9 offset:4096
	ds_read_b32 v197, v9 offset:4608
	ds_read_b32 v198, v9 offset:5120
	ds_read_b32 v199, v9 offset:5632
	ds_read_b32 v200, v9 offset:6144
	ds_read_b32 v201, v9 offset:6656
	ds_read_b32 v202, v9 offset:7168
	ds_read_b32 v203, v9 offset:7680
	s_waitcnt lgkmcnt(0)
	v_max_f32_e32 v170, v170, v170
	v_max_f32_e32 v171, v171, v171
	v_max_f32_e32 v172, v172, v172
	v_max_f32_e32 v173, v173, v173
	v_max_f32_e32 v174, v174, v174
	v_max_f32_e32 v175, v175, v175
	v_max_f32_e32 v176, v176, v176
	v_max_f32_e32 v177, v177, v177
	v_max_f32_e32 v196, v196, v196
	v_max_f32_e32 v197, v197, v197
	v_max_f32_e32 v198, v198, v198
	v_max_f32_e32 v199, v199, v199
	v_max_f32_e32 v200, v200, v200
	v_max_f32_e32 v201, v201, v201
	v_max_f32_e32 v202, v202, v202
	v_max_f32_e32 v203, v203, v203
	v_med3_f32 v170, v170, s20, v13
	v_med3_f32 v171, v171, s20, v13
	v_med3_f32 v172, v172, s20, v13
	v_med3_f32 v173, v173, s20, v13
	v_med3_f32 v174, v174, s20, v13
	v_med3_f32 v175, v175, s20, v13
	v_med3_f32 v176, v176, s20, v13
	v_med3_f32 v177, v177, s20, v13
	v_med3_f32 v196, v196, s20, v13
	v_med3_f32 v197, v197, s20, v13
	v_med3_f32 v198, v198, s20, v13
	v_med3_f32 v199, v199, s20, v13
	v_med3_f32 v200, v200, s20, v13
	v_med3_f32 v201, v201, s20, v13
	v_med3_f32 v202, v202, s20, v13
	v_med3_f32 v203, v203, s20, v13
	v_mov_b32_e32 v208, 0
	v_mov_b32_e32 v209, 0
	v_mov_b32_e32 v210, 0
	v_mov_b32_e32 v211, 0
	v_cvt_pk_fp8_f32 v208, v170, v171
	v_cvt_pk_fp8_f32 v209, v174, v175
	v_cvt_pk_fp8_f32 v210, v196, v197
	v_cvt_pk_fp8_f32 v211, v200, v201
	v_cvt_pk_fp8_f32 v208, v172, v173 op_sel:[0,0,1]
	v_cvt_pk_fp8_f32 v209, v176, v177 op_sel:[0,0,1]
	v_cvt_pk_fp8_f32 v210, v198, v199 op_sel:[0,0,1]
	v_cvt_pk_fp8_f32 v211, v202, v203 op_sel:[0,0,1]
	s_nop 0
	global_store_dwordx4 v29, v[208:211], s[14:15]
	s_waitcnt vmcnt(32)
	v_mul_f32_e32 v36, v20, v36
	v_mul_f32_e32 v37, v20, v37
	v_mul_f32_e32 v38, v20, v38
	v_mul_f32_e32 v39, v20, v39
	ds_write_b128 v4, v[36:39]
	v_mul_f32_e32 v40, v21, v40
	v_mul_f32_e32 v41, v21, v41
	v_mul_f32_e32 v42, v21, v42
	v_mul_f32_e32 v43, v21, v43
	ds_write_b128 v4, v[40:43] offset:1024
	v_mul_f32_e32 v44, v22, v44
	v_mul_f32_e32 v45, v22, v45
	v_mul_f32_e32 v46, v22, v46
	v_mul_f32_e32 v47, v22, v47
	ds_write_b128 v4, v[44:47] offset:2048
	v_mul_f32_e32 v48, v23, v48
	v_mul_f32_e32 v49, v23, v49
	v_mul_f32_e32 v50, v23, v50
	v_mul_f32_e32 v51, v23, v51
	ds_write_b128 v4, v[48:51] offset:3072
	v_mul_f32_e32 v52, v24, v52
	v_mul_f32_e32 v53, v24, v53
	v_mul_f32_e32 v54, v24, v54
	v_mul_f32_e32 v55, v24, v55
	ds_write_b128 v4, v[52:55] offset:4096
	v_mul_f32_e32 v56, v25, v56
	v_mul_f32_e32 v57, v25, v57
	v_mul_f32_e32 v58, v25, v58
	v_mul_f32_e32 v59, v25, v59
	ds_write_b128 v4, v[56:59] offset:5120
	v_mul_f32_e32 v60, v26, v60
	v_mul_f32_e32 v61, v26, v61
	v_mul_f32_e32 v62, v26, v62
	v_mul_f32_e32 v63, v26, v63
	ds_write_b128 v4, v[60:63] offset:6144
	v_mul_f32_e32 v64, v27, v64
	v_mul_f32_e32 v65, v27, v65
	v_mul_f32_e32 v66, v27, v66
	v_mul_f32_e32 v67, v27, v67
	ds_write_b128 v4, v[64:67] offset:7168
	s_waitcnt lgkmcnt(0)
	s_barrier
; #define GAS __attribute__((address_space(1)))
; #define LAS __attribute__((address_space(3)))
; #define LDS_WAIT() asm volatile("s_waitcnt lgkmcnt(0)" ::: "memory")
;     const int pr = item >> 1, kb = 2 * (pr / nblk) + (item & 1), nb = pr % nblk, k0 = 64 * kb, n0 = 32 * nb;
;     const int nr = n0 + (lane & 31); const int sc = MAP == 1 ? src_col_in(nr) : nr;
;     float v[32];
; #pragma unroll
;     for (int i = 0; i < 32; ++i) v[i] = sc >= 0 ? W[(size_t)(k0 + 2 * i + (lane >> 5)) * Nsrc + sc] : 0.f;
; #pragma unroll
;     for (int i = 0; i < 32; ++i) { const int k = k0 + 2 * i + (lane >> 5); float x = v[i] * wscale; if (KS) x *= (k < ksplit ? ksA[k] : ksB[k - ksplit]); scr[(2 * i + (lane >> 5)) * 33 + (lane & 31)] = x; }
;     LDS_WAIT(); asm volatile("" ::: "memory");
;     const int c = lane & 7;
; #pragma unroll
;     for (int j = 0; j < 4; ++j) { const int n = (lane >> 3) + 8 * j; const LAS float* s = scr + (8 * c) * 33 + n;
;         const unsigned long long o = (unsigned long long)pg8::pk4_fp8(s[0 * 33], s[1 * 33], s[2 * 33], s[3 * 33]) | ((unsigned long long)pg8::pk4_fp8(s[4 * 33], s[5 * 33], s[6 * 33], s[7 * 33]) << 32);
;         *(GAS unsigned long long*)(WT + (size_t)(n0 + n) * K + k0 + 8 * c) = o; }
;     LDS_WAIT(); asm volatile("" ::: "memory");
; __global__ void __launch_bounds__(NWAVES * 64, 2) hybrid_fwd(Args args) {
;     ...
;             if (r < I_O) { if (l >= WO_F8_FROM) p0_transpose_item_f8<true>(args.in[13] + (size_t)l * DM * DM, DM, DM, DM / 32, (unsigned char*)(ws + WS_WO + l * SZ_WO), 64.f, args.in[6] + l * 2048, args.in[12] + l * 2048, 2048, scr, r, lane);
;                 else p0_transpose_item<0, true>(args.in[13] + (size_t)l * DM * DM, DM, DM, DM / 32, (bf16*)(ws + WS_WO + l * SZ_WO), args.in[6] + l * 2048, args.in[12] + l * 2048, 2048, scr, r, lane); continue; } r -= I_O;
;             if (r < I_UP) { p0_transpose_item_f8<true>(args.in[15] + (size_t)l * DM * FF, DM, FF, FF / 32, (unsigned char*)(ws + WS_WUP + l * SZ_WUP), WUP8_SCALE, args.in[14] + l * DM, args.in[14] + l * DM, DM, scr, r, lane); continue; } r -= I_UP;
;             p0_transpose_item_f8<false>(args.in[16] + (size_t)l * FF * DM, FF, DM, DM / 32, (unsigned char*)(ws + WS_WDN + l * SZ_WDN), 128.f, args.in[16], args.in[16], 0, scr, r, lane);
	s_add_i32 s19, s39, 15
	s_min_u32 s19, s19, 31
	s_lshl_b32 s19, s19, 9
	s_add_u32 s12, s22, s19
	s_addc_u32 s13, s23, 0
	global_load_dwordx4 v[36:39], v10, s[12:13]
	s_add_u32 s12, s12, 0x8000
	s_addc_u32 s13, s13, 0
	global_load_dwordx4 v[40:43], v10, s[12:13]
	s_add_u32 s12, s12, 0x8000
	s_addc_u32 s13, s13, 0
	global_load_dwordx4 v[44:47], v10, s[12:13]
	s_add_u32 s12, s12, 0x8000
	s_addc_u32 s13, s13, 0
	global_load_dwordx4 v[48:51], v10, s[12:13]
	s_add_u32 s12, s12, 0x8000
	s_addc_u32 s13, s13, 0
	global_load_dwordx4 v[52:55], v10, s[12:13]
	s_add_u32 s12, s12, 0x8000
	s_addc_u32 s13, s13, 0
	global_load_dwordx4 v[56:59], v10, s[12:13]
	s_add_u32 s12, s12, 0x8000
	s_addc_u32 s13, s13, 0
	global_load_dwordx4 v[60:63], v10, s[12:13]
	s_add_u32 s12, s12, 0x8000
	s_addc_u32 s13, s13, 0
	global_load_dwordx4 v[64:67], v10, s[12:13]
	s_add_i32 s19, s39, 3
	s_min_u32 s19, s19, 31
	s_lshl_b32 s19, s19, 19
	s_add_u32 s14, s50, s19
	s_addc_u32 s15, s51, 0
	ds_read_b32 v170, v6
	ds_read_b32 v171, v6 offset:512
	ds_read_b32 v172, v6 offset:1024
	ds_read_b32 v173, v6 offset:1536
	ds_read_b32 v174, v6 offset:2048
	ds_read_b32 v175, v6 offset:2560
	ds_read_b32 v176, v6 offset:3072
	ds_read_b32 v177, v6 offset:3584
	ds_read_b32 v196, v6 offset:4096
	ds_read_b32 v197, v6 offset:4608
	ds_read_b32 v198, v6 offset:5120
	ds_read_b32 v199, v6 offset:5632
	ds_read_b32 v200, v6 offset:6144
	ds_read_b32 v201, v6 offset:6656
	ds_read_b32 v202, v6 offset:7168
	ds_read_b32 v203, v6 offset:7680
	s_waitcnt lgkmcnt(0)
	v_max_f32_e32 v170, v170, v170
	v_max_f32_e32 v171, v171, v171
	v_max_f32_e32 v172, v172, v172
	v_max_f32_e32 v173, v173, v173
	v_max_f32_e32 v174, v174, v174
	v_max_f32_e32 v175, v175, v175
	v_max_f32_e32 v176, v176, v176
	v_max_f32_e32 v177, v177, v177
	v_max_f32_e32 v196, v196, v196
	v_max_f32_e32 v197, v197, v197
	v_max_f32_e32 v198, v198, v198
	v_max_f32_e32 v199, v199, v199
	v_max_f32_e32 v200, v200, v200
	v_max_f32_e32 v201, v201, v201
	v_max_f32_e32 v202, v202, v202
	v_max_f32_e32 v203, v203, v203
	v_med3_f32 v170, v170, s20, v13
	v_med3_f32 v171, v171, s20, v13
	v_med3_f32 v172, v172, s20, v13
	v_med3_f32 v173, v173, s20, v13
	v_med3_f32 v174, v174, s20, v13
	v_med3_f32 v175, v175, s20, v13
	v_med3_f32 v176, v176, s20, v13
	v_med3_f32 v177, v177, s20, v13
	v_med3_f32 v196, v196, s20, v13
	v_med3_f32 v197, v197, s20, v13
	v_med3_f32 v198, v198, s20, v13
	v_med3_f32 v199, v199, s20, v13
	v_med3_f32 v200, v200, s20, v13
	v_med3_f32 v201, v201, s20, v13
	v_med3_f32 v202, v202, s20, v13
	v_med3_f32 v203, v203, s20, v13
	v_mov_b32_e32 v208, 0
	v_mov_b32_e32 v209, 0
	v_mov_b32_e32 v210, 0
	v_mov_b32_e32 v211, 0
	v_cvt_pk_fp8_f32 v208, v170, v171
	v_cvt_pk_fp8_f32 v209, v174, v175
	v_cvt_pk_fp8_f32 v210, v196, v197
	v_cvt_pk_fp8_f32 v211, v200, v201
	v_cvt_pk_fp8_f32 v208, v172, v173 op_sel:[0,0,1]
	v_cvt_pk_fp8_f32 v209, v176, v177 op_sel:[0,0,1]
	v_cvt_pk_fp8_f32 v210, v198, v199 op_sel:[0,0,1]
	v_cvt_pk_fp8_f32 v211, v202, v203 op_sel:[0,0,1]
	s_nop 0
	global_store_dwordx4 v28, v[208:211], s[14:15]
	ds_read_b32 v170, v8
	ds_read_b32 v171, v8 offset:512
	ds_read_b32 v172, v8 offset:1024
	ds_read_b32 v173, v8 offset:1536
	ds_read_b32 v174, v8 offset:2048
	ds_read_b32 v175, v8 offset:2560
	ds_read_b32 v176, v8 offset:3072
	ds_read_b32 v177, v8 offset:3584
	ds_read_b32 v196, v8 offset:4096
	ds_read_b32 v197, v8 offset:4608
	ds_read_b32 v198, v8 offset:5120
	ds_read_b32 v199, v8 offset:5632
	ds_read_b32 v200, v8 offset:6144
	ds_read_b32 v201, v8 offset:6656
	ds_read_b32 v202, v8 offset:7168
	ds_read_b32 v203, v8 offset:7680
	s_waitcnt lgkmcnt(0)
	v_max_f32_e32 v170, v170, v170
	v_max_f32_e32 v171, v171, v171
	v_max_f32_e32 v172, v172, v172
	v_max_f32_e32 v173, v173, v173
	v_max_f32_e32 v174, v174, v174
	v_max_f32_e32 v175, v175, v175
	v_max_f32_e32 v176, v176, v176
	v_max_f32_e32 v177, v177, v177
	v_max_f32_e32 v196, v196, v196
	v_max_f32_e32 v197, v197, v197
	v_max_f32_e32 v198, v198, v198
	v_max_f32_e32 v199, v199, v199
	v_max_f32_e32 v200, v200, v200
	v_max_f32_e32 v201, v201, v201
	v_max_f32_e32 v202, v202, v202
	v_max_f32_e32 v203, v203, v203
	v_med3_f32 v170, v170, s20, v13
	v_med3_f32 v171, v171, s20, v13
	v_med3_f32 v172, v172, s20, v13
	v_med3_f32 v173, v173, s20, v13
	v_med3_f32 v174, v174, s20, v13
	v_med3_f32 v175, v175, s20, v13
	v_med3_f32 v176, v176, s20, v13
	v_med3_f32 v177, v177, s20, v13
	v_med3_f32 v196, v196, s20, v13
	v_med3_f32 v197, v197, s20, v13
	v_med3_f32 v198, v198, s20, v13
	v_med3_f32 v199, v199, s20, v13
	v_med3_f32 v200, v200, s20, v13
	v_med3_f32 v201, v201, s20, v13
	v_med3_f32 v202, v202, s20, v13
	v_med3_f32 v203, v203, s20, v13
	v_mov_b32_e32 v208, 0
	v_mov_b32_e32 v209, 0
	v_mov_b32_e32 v210, 0
	v_mov_b32_e32 v211, 0
	v_cvt_pk_fp8_f32 v208, v170, v171
	v_cvt_pk_fp8_f32 v209, v174, v175
	v_cvt_pk_fp8_f32 v210, v196, v197
	v_cvt_pk_fp8_f32 v211, v200, v201
	v_cvt_pk_fp8_f32 v208, v172, v173 op_sel:[0,0,1]
	v_cvt_pk_fp8_f32 v209, v176, v177 op_sel:[0,0,1]
	v_cvt_pk_fp8_f32 v210, v198, v199 op_sel:[0,0,1]
	v_cvt_pk_fp8_f32 v211, v202, v203 op_sel:[0,0,1]
	s_nop 0
	global_store_dwordx4 v29, v[208:211], s[14:15]
	s_waitcnt vmcnt(32)
	v_mul_f32_e32 v68, v20, v68
	v_mul_f32_e32 v69, v20, v69
	v_mul_f32_e32 v70, v20, v70
	v_mul_f32_e32 v71, v20, v71
	ds_write_b128 v5, v[68:71]
	v_mul_f32_e32 v72, v21, v72
	v_mul_f32_e32 v73, v21, v73
	v_mul_f32_e32 v74, v21, v74
	v_mul_f32_e32 v75, v21, v75
	ds_write_b128 v5, v[72:75] offset:1024
	v_mul_f32_e32 v76, v22, v76
	v_mul_f32_e32 v77, v22, v77
	v_mul_f32_e32 v78, v22, v78
	v_mul_f32_e32 v79, v22, v79
	ds_write_b128 v5, v[76:79] offset:2048
	v_mul_f32_e32 v80, v23, v80
	v_mul_f32_e32 v81, v23, v81
	v_mul_f32_e32 v82, v23, v82
	v_mul_f32_e32 v83, v23, v83
	ds_write_b128 v5, v[80:83] offset:3072
	v_mul_f32_e32 v84, v24, v84
	v_mul_f32_e32 v85, v24, v85
	v_mul_f32_e32 v86, v24, v86
	v_mul_f32_e32 v87, v24, v87
	ds_write_b128 v5, v[84:87] offset:4096
	v_mul_f32_e32 v88, v25, v88
	v_mul_f32_e32 v89, v25, v89
	v_mul_f32_e32 v90, v25, v90
	v_mul_f32_e32 v91, v25, v91
	ds_write_b128 v5, v[88:91] offset:5120
	v_mul_f32_e32 v92, v26, v92
	v_mul_f32_e32 v93, v26, v93
	v_mul_f32_e32 v94, v26, v94
	v_mul_f32_e32 v95, v26, v95
	ds_write_b128 v5, v[92:95] offset:6144
	v_mul_f32_e32 v96, v27, v96
	v_mul_f32_e32 v97, v27, v97
	v_mul_f32_e32 v98, v27, v98
	v_mul_f32_e32 v99, v27, v99
	ds_write_b128 v5, v[96:99] offset:7168
	s_waitcnt lgkmcnt(0)
	s_barrier
; #define GAS __attribute__((address_space(1)))
; #define LAS __attribute__((address_space(3)))
; #define LDS_WAIT() asm volatile("s_waitcnt lgkmcnt(0)" ::: "memory")
;     const int pr = item >> 1, kb = 2 * (pr / nblk) + (item & 1), nb = pr % nblk, k0 = 64 * kb, n0 = 32 * nb;
;     const int nr = n0 + (lane & 31); const int sc = MAP == 1 ? src_col_in(nr) : nr;
;     float v[32];
; #pragma unroll
;     for (int i = 0; i < 32; ++i) v[i] = sc >= 0 ? W[(size_t)(k0 + 2 * i + (lane >> 5)) * Nsrc + sc] : 0.f;
; #pragma unroll
;     for (int i = 0; i < 32; ++i) { const int k = k0 + 2 * i + (lane >> 5); float x = v[i] * wscale; if (KS) x *= (k < ksplit ? ksA[k] : ksB[k - ksplit]); scr[(2 * i + (lane >> 5)) * 33 + (lane & 31)] = x; }
;     LDS_WAIT(); asm volatile("" ::: "memory");
;     const int c = lane & 7;
; #pragma unroll
;     for (int j = 0; j < 4; ++j) { const int n = (lane >> 3) + 8 * j; const LAS float* s = scr + (8 * c) * 33 + n;
;         const unsigned long long o = (unsigned long long)pg8::pk4_fp8(s[0 * 33], s[1 * 33], s[2 * 33], s[3 * 33]) | ((unsigned long long)pg8::pk4_fp8(s[4 * 33], s[5 * 33], s[6 * 33], s[7 * 33]) << 32);
;         *(GAS unsigned long long*)(WT + (size_t)(n0 + n) * K + k0 + 8 * c) = o; }
;     LDS_WAIT(); asm volatile("" ::: "memory");
; __global__ void __launch_bounds__(NWAVES * 64, 2) hybrid_fwd(Args args) {
;     ...
;             if (r < I_O) { if (l >= WO_F8_FROM) p0_transpose_item_f8<true>(args.in[13] + (size_t)l * DM * DM, DM, DM, DM / 32, (unsigned char*)(ws + WS_WO + l * SZ_WO), 64.f, args.in[6] + l * 2048, args.in[12] + l * 2048, 2048, scr, r, lane);
;                 else p0_transpose_item<0, true>(args.in[13] + (size_t)l * DM * DM, DM, DM, DM / 32, (bf16*)(ws + WS_WO + l * SZ_WO), args.in[6] + l * 2048, args.in[12] + l * 2048, 2048, scr, r, lane); continue; } r -= I_O;
;             if (r < I_UP) { p0_transpose_item_f8<true>(args.in[15] + (size_t)l * DM * FF, DM, FF, FF / 32, (unsigned char*)(ws + WS_WUP + l * SZ_WUP), WUP8_SCALE, args.in[14] + l * DM, args.in[14] + l * DM, DM, scr, r, lane); continue; } r -= I_UP;
;             p0_transpose_item_f8<false>(args.in[16] + (size_t)l * FF * DM, FF, DM, DM / 32, (unsigned char*)(ws + WS_WDN + l * SZ_WDN), 128.f, args.in[16], args.in[16], 0, scr, r, lane);
	s_add_i32 s19, s39, 18
	s_min_u32 s19, s19, 31
	s_lshl_b32 s19, s19, 9
	s_add_u32 s12, s22, s19
	s_addc_u32 s13, s23, 0
	global_load_dwordx4 v[68:71], v10, s[12:13]
	s_add_u32 s12, s12, 0x8000
	s_addc_u32 s13, s13, 0
	global_load_dwordx4 v[72:75], v10, s[12:13]
	s_add_u32 s12, s12, 0x8000
	s_addc_u32 s13, s13, 0
	global_load_dwordx4 v[76:79], v10, s[12:13]
	s_add_u32 s12, s12, 0x8000
	s_addc_u32 s13, s13, 0
	global_load_dwordx4 v[80:83], v10, s[12:13]
	s_add_u32 s12, s12, 0x8000
	s_addc_u32 s13, s13, 0
	global_load_dwordx4 v[84:87], v10, s[12:13]
	s_add_u32 s12, s12, 0x8000
	s_addc_u32 s13, s13, 0
	global_load_dwordx4 v[88:91], v10, s[12:13]
	s_add_u32 s12, s12, 0x8000
	s_addc_u32 s13, s13, 0
	global_load_dwordx4 v[92:95], v10, s[12:13]
	s_add_u32 s12, s12, 0x8000
	s_addc_u32 s13, s13, 0
	global_load_dwordx4 v[96:99], v10, s[12:13]
	s_add_i32 s19, s39, 6
	s_min_u32 s19, s19, 31
	s_lshl_b32 s19, s19, 19
	s_add_u32 s14, s50, s19
	s_addc_u32 s15, s51, 0
	ds_read_b32 v170, v7
	ds_read_b32 v171, v7 offset:512
	ds_read_b32 v172, v7 offset:1024
	ds_read_b32 v173, v7 offset:1536
	ds_read_b32 v174, v7 offset:2048
	ds_read_b32 v175, v7 offset:2560
	ds_read_b32 v176, v7 offset:3072
	ds_read_b32 v177, v7 offset:3584
	ds_read_b32 v196, v7 offset:4096
	ds_read_b32 v197, v7 offset:4608
	ds_read_b32 v198, v7 offset:5120
	ds_read_b32 v199, v7 offset:5632
	ds_read_b32 v200, v7 offset:6144
	ds_read_b32 v201, v7 offset:6656
	ds_read_b32 v202, v7 offset:7168
	ds_read_b32 v203, v7 offset:7680
	s_waitcnt lgkmcnt(0)
	v_max_f32_e32 v170, v170, v170
	v_max_f32_e32 v171, v171, v171
	v_max_f32_e32 v172, v172, v172
	v_max_f32_e32 v173, v173, v173
	v_max_f32_e32 v174, v174, v174
	v_max_f32_e32 v175, v175, v175
	v_max_f32_e32 v176, v176, v176
	v_max_f32_e32 v177, v177, v177
	v_max_f32_e32 v196, v196, v196
	v_max_f32_e32 v197, v197, v197
	v_max_f32_e32 v198, v198, v198
	v_max_f32_e32 v199, v199, v199
	v_max_f32_e32 v200, v200, v200
	v_max_f32_e32 v201, v201, v201
	v_max_f32_e32 v202, v202, v202
	v_max_f32_e32 v203, v203, v203
	v_med3_f32 v170, v170, s20, v13
	v_med3_f32 v171, v171, s20, v13
	v_med3_f32 v172, v172, s20, v13
	v_med3_f32 v173, v173, s20, v13
	v_med3_f32 v174, v174, s20, v13
	v_med3_f32 v175, v175, s20, v13
	v_med3_f32 v176, v176, s20, v13
	v_med3_f32 v177, v177, s20, v13
	v_med3_f32 v196, v196, s20, v13
	v_med3_f32 v197, v197, s20, v13
	v_med3_f32 v198, v198, s20, v13
	v_med3_f32 v199, v199, s20, v13
	v_med3_f32 v200, v200, s20, v13
	v_med3_f32 v201, v201, s20, v13
	v_med3_f32 v202, v202, s20, v13
	v_med3_f32 v203, v203, s20, v13
	v_mov_b32_e32 v208, 0
	v_mov_b32_e32 v209, 0
	v_mov_b32_e32 v210, 0
	v_mov_b32_e32 v211, 0
	v_cvt_pk_fp8_f32 v208, v170, v171
	v_cvt_pk_fp8_f32 v209, v174, v175
	v_cvt_pk_fp8_f32 v210, v196, v197
	v_cvt_pk_fp8_f32 v211, v200, v201
	v_cvt_pk_fp8_f32 v208, v172, v173 op_sel:[0,0,1]
	v_cvt_pk_fp8_f32 v209, v176, v177 op_sel:[0,0,1]
	v_cvt_pk_fp8_f32 v210, v198, v199 op_sel:[0,0,1]
	v_cvt_pk_fp8_f32 v211, v202, v203 op_sel:[0,0,1]
	s_nop 0
	global_store_dwordx4 v28, v[208:211], s[14:15]
	ds_read_b32 v170, v9
	ds_read_b32 v171, v9 offset:512
	ds_read_b32 v172, v9 offset:1024
	ds_read_b32 v173, v9 offset:1536
	ds_read_b32 v174, v9 offset:2048
	ds_read_b32 v175, v9 offset:2560
	ds_read_b32 v176, v9 offset:3072
	ds_read_b32 v177, v9 offset:3584
	ds_read_b32 v196, v9 offset:4096
	ds_read_b32 v197, v9 offset:4608
	ds_read_b32 v198, v9 offset:5120
	ds_read_b32 v199, v9 offset:5632
	ds_read_b32 v200, v9 offset:6144
	ds_read_b32 v201, v9 offset:6656
	ds_read_b32 v202, v9 offset:7168
	ds_read_b32 v203, v9 offset:7680
	s_waitcnt lgkmcnt(0)
	v_max_f32_e32 v170, v170, v170
	v_max_f32_e32 v171, v171, v171
	v_max_f32_e32 v172, v172, v172
	v_max_f32_e32 v173, v173, v173
	v_max_f32_e32 v174, v174, v174
	v_max_f32_e32 v175, v175, v175
	v_max_f32_e32 v176, v176, v176
	v_max_f32_e32 v177, v177, v177
	v_max_f32_e32 v196, v196, v196
	v_max_f32_e32 v197, v197, v197
	v_max_f32_e32 v198, v198, v198
	v_max_f32_e32 v199, v199, v199
	v_max_f32_e32 v200, v200, v200
	v_max_f32_e32 v201, v201, v201
	v_max_f32_e32 v202, v202, v202
	v_max_f32_e32 v203, v203, v203
	v_med3_f32 v170, v170, s20, v13
	v_med3_f32 v171, v171, s20, v13
	v_med3_f32 v172, v172, s20, v13
	v_med3_f32 v173, v173, s20, v13
	v_med3_f32 v174, v174, s20, v13
	v_med3_f32 v175, v175, s20, v13
	v_med3_f32 v176, v176, s20, v13
	v_med3_f32 v177, v177, s20, v13
	v_med3_f32 v196, v196, s20, v13
	v_med3_f32 v197, v197, s20, v13
	v_med3_f32 v198, v198, s20, v13
	v_med3_f32 v199, v199, s20, v13
	v_med3_f32 v200, v200, s20, v13
	v_med3_f32 v201, v201, s20, v13
	v_med3_f32 v202, v202, s20, v13
	v_med3_f32 v203, v203, s20, v13
	v_mov_b32_e32 v208, 0
	v_mov_b32_e32 v209, 0
	v_mov_b32_e32 v210, 0
	v_mov_b32_e32 v211, 0
	v_cvt_pk_fp8_f32 v208, v170, v171
	v_cvt_pk_fp8_f32 v209, v174, v175
	v_cvt_pk_fp8_f32 v210, v196, v197
	v_cvt_pk_fp8_f32 v211, v200, v201
	v_cvt_pk_fp8_f32 v208, v172, v173 op_sel:[0,0,1]
	v_cvt_pk_fp8_f32 v209, v176, v177 op_sel:[0,0,1]
	v_cvt_pk_fp8_f32 v210, v198, v199 op_sel:[0,0,1]
	v_cvt_pk_fp8_f32 v211, v202, v203 op_sel:[0,0,1]
	s_nop 0
	global_store_dwordx4 v29, v[208:211], s[14:15]
	s_waitcnt vmcnt(32)
	v_mul_f32_e32 v100, v20, v100
	v_mul_f32_e32 v101, v20, v101
	v_mul_f32_e32 v102, v20, v102
	v_mul_f32_e32 v103, v20, v103
	ds_write_b128 v4, v[100:103]
	v_mul_f32_e32 v104, v21, v104
	v_mul_f32_e32 v105, v21, v105
	v_mul_f32_e32 v106, v21, v106
	v_mul_f32_e32 v107, v21, v107
	ds_write_b128 v4, v[104:107] offset:1024
	v_mul_f32_e32 v108, v22, v108
	v_mul_f32_e32 v109, v22, v109
	v_mul_f32_e32 v110, v22, v110
	v_mul_f32_e32 v111, v22, v111
	ds_write_b128 v4, v[108:111] offset:2048
	v_mul_f32_e32 v112, v23, v112
	v_mul_f32_e32 v113, v23, v113
	v_mul_f32_e32 v114, v23, v114
	v_mul_f32_e32 v115, v23, v115
	ds_write_b128 v4, v[112:115] offset:3072
	v_mul_f32_e32 v116, v24, v116
	v_mul_f32_e32 v117, v24, v117
	v_mul_f32_e32 v118, v24, v118
	v_mul_f32_e32 v119, v24, v119
	ds_write_b128 v4, v[116:119] offset:4096
	v_mul_f32_e32 v120, v25, v120
	v_mul_f32_e32 v121, v25, v121
	v_mul_f32_e32 v122, v25, v122
	v_mul_f32_e32 v123, v25, v123
	ds_write_b128 v4, v[120:123] offset:5120
	v_mul_f32_e32 v124, v26, v124
	v_mul_f32_e32 v125, v26, v125
	v_mul_f32_e32 v126, v26, v126
	v_mul_f32_e32 v127, v26, v127
	ds_write_b128 v4, v[124:127] offset:6144
	v_mul_f32_e32 v128, v27, v128
	v_mul_f32_e32 v129, v27, v129
	v_mul_f32_e32 v130, v27, v130
	v_mul_f32_e32 v131, v27, v131
	ds_write_b128 v4, v[128:131] offset:7168
	s_waitcnt lgkmcnt(0)
	s_barrier
; #define GAS __attribute__((address_space(1)))
; #define LAS __attribute__((address_space(3)))
; #define LDS_WAIT() asm volatile("s_waitcnt lgkmcnt(0)" ::: "memory")
;     const int pr = item >> 1, kb = 2 * (pr / nblk) + (item & 1), nb = pr % nblk, k0 = 64 * kb, n0 = 32 * nb;
;     const int nr = n0 + (lane & 31); const int sc = MAP == 1 ? src_col_in(nr) : nr;
;     float v[32];
; #pragma unroll
;     for (int i = 0; i < 32; ++i) v[i] = sc >= 0 ? W[(size_t)(k0 + 2 * i + (lane >> 5)) * Nsrc + sc] : 0.f;
; #pragma unroll
;     for (int i = 0; i < 32; ++i) { const int k = k0 + 2 * i + (lane >> 5); float x = v[i] * wscale; if (KS) x *= (k < ksplit ? ksA[k] : ksB[k - ksplit]); scr[(2 * i + (lane >> 5)) * 33 + (lane & 31)] = x; }
;     LDS_WAIT(); asm volatile("" ::: "memory");
;     const int c = lane & 7;
; #pragma unroll
;     for (int j = 0; j < 4; ++j) { const int n = (lane >> 3) + 8 * j; const LAS float* s = scr + (8 * c) * 33 + n;
;         const unsigned long long o = (unsigned long long)pg8::pk4_fp8(s[0 * 33], s[1 * 33], s[2 * 33], s[3 * 33]) | ((unsigned long long)pg8::pk4_fp8(s[4 * 33], s[5 * 33], s[6 * 33], s[7 * 33]) << 32);
;         *(GAS unsigned long long*)(WT + (size_t)(n0 + n) * K + k0 + 8 * c) = o; }
;     LDS_WAIT(); asm volatile("" ::: "memory");
; __global__ void __launch_bounds__(NWAVES * 64, 2) hybrid_fwd(Args args) {
;     ...
;             if (r < I_O) { if (l >= WO_F8_FROM) p0_transpose_item_f8<true>(args.in[13] + (size_t)l * DM * DM, DM, DM, DM / 32, (unsigned char*)(ws + WS_WO + l * SZ_WO), 64.f, args.in[6] + l * 2048, args.in[12] + l * 2048, 2048, scr, r, lane);
;                 else p0_transpose_item<0, true>(args.in[13] + (size_t)l * DM * DM, DM, DM, DM / 32, (bf16*)(ws + WS_WO + l * SZ_WO), args.in[6] + l * 2048, args.in[12] + l * 2048, 2048, scr, r, lane); continue; } r -= I_O;
;             if (r < I_UP) { p0_transpose_item_f8<true>(args.in[15] + (size_t)l * DM * FF, DM, FF, FF / 32, (unsigned char*)(ws + WS_WUP + l * SZ_WUP), WUP8_SCALE, args.in[14] + l * DM, args.in[14] + l * DM, DM, scr, r, lane); continue; } r -= I_UP;
;             p0_transpose_item_f8<false>(args.in[16] + (size_t)l * FF * DM, FF, DM, DM / 32, (unsigned char*)(ws + WS_WDN + l * SZ_WDN), 128.f, args.in[16], args.in[16], 0, scr, r, lane);
	s_add_i32 s19, s39, 21
	s_min_u32 s19, s19, 31
	s_lshl_b32 s19, s19, 9
	s_add_u32 s12, s22, s19
	s_addc_u32 s13, s23, 0
	global_load_dwordx4 v[100:103], v10, s[12:13]
	s_add_u32 s12, s12, 0x8000
	s_addc_u32 s13, s13, 0
	global_load_dwordx4 v[104:107], v10, s[12:13]
	s_add_u32 s12, s12, 0x8000
	s_addc_u32 s13, s13, 0
	global_load_dwordx4 v[108:111], v10, s[12:13]
	s_add_u32 s12, s12, 0x8000
	s_addc_u32 s13, s13, 0
	global_load_dwordx4 v[112:115], v10, s[12:13]
	s_add_u32 s12, s12, 0x8000
	s_addc_u32 s13, s13, 0
	global_load_dwordx4 v[116:119], v10, s[12:13]
	s_add_u32 s12, s12, 0x8000
	s_addc_u32 s13, s13, 0
	global_load_dwordx4 v[120:123], v10, s[12:13]
	s_add_u32 s12, s12, 0x8000
	s_addc_u32 s13, s13, 0
	global_load_dwordx4 v[124:127], v10, s[12:13]
	s_add_u32 s12, s12, 0x8000
	s_addc_u32 s13, s13, 0
	global_load_dwordx4 v[128:131], v10, s[12:13]
	s_add_i32 s19, s39, 9
	s_min_u32 s19, s19, 31
	s_lshl_b32 s19, s19, 19
	s_add_u32 s14, s50, s19
	s_addc_u32 s15, s51, 0
	ds_read_b32 v170, v6
	ds_read_b32 v171, v6 offset:512
	ds_read_b32 v172, v6 offset:1024
	ds_read_b32 v173, v6 offset:1536
	ds_read_b32 v174, v6 offset:2048
	ds_read_b32 v175, v6 offset:2560
	ds_read_b32 v176, v6 offset:3072
	ds_read_b32 v177, v6 offset:3584
	ds_read_b32 v196, v6 offset:4096
	ds_read_b32 v197, v6 offset:4608
	ds_read_b32 v198, v6 offset:5120
	ds_read_b32 v199, v6 offset:5632
	ds_read_b32 v200, v6 offset:6144
	ds_read_b32 v201, v6 offset:6656
	ds_read_b32 v202, v6 offset:7168
	ds_read_b32 v203, v6 offset:7680
	s_waitcnt lgkmcnt(0)
	v_max_f32_e32 v170, v170, v170
	v_max_f32_e32 v171, v171, v171
	v_max_f32_e32 v172, v172, v172
	v_max_f32_e32 v173, v173, v173
	v_max_f32_e32 v174, v174, v174
	v_max_f32_e32 v175, v175, v175
	v_max_f32_e32 v176, v176, v176
	v_max_f32_e32 v177, v177, v177
	v_max_f32_e32 v196, v196, v196
	v_max_f32_e32 v197, v197, v197
	v_max_f32_e32 v198, v198, v198
	v_max_f32_e32 v199, v199, v199
	v_max_f32_e32 v200, v200, v200
	v_max_f32_e32 v201, v201, v201
	v_max_f32_e32 v202, v202, v202
	v_max_f32_e32 v203, v203, v203
	v_med3_f32 v170, v170, s20, v13
	v_med3_f32 v171, v171, s20, v13
	v_med3_f32 v172, v172, s20, v13
	v_med3_f32 v173, v173, s20, v13
	v_med3_f32 v174, v174, s20, v13
	v_med3_f32 v175, v175, s20, v13
	v_med3_f32 v176, v176, s20, v13
	v_med3_f32 v177, v177, s20, v13
	v_med3_f32 v196, v196, s20, v13
	v_med3_f32 v197, v197, s20, v13
	v_med3_f32 v198, v198, s20, v13
	v_med3_f32 v199, v199, s20, v13
	v_med3_f32 v200, v200, s20, v13
	v_med3_f32 v201, v201, s20, v13
	v_med3_f32 v202, v202, s20, v13
	v_med3_f32 v203, v203, s20, v13
	v_mov_b32_e32 v208, 0
	v_mov_b32_e32 v209, 0
	v_mov_b32_e32 v210, 0
	v_mov_b32_e32 v211, 0
	v_cvt_pk_fp8_f32 v208, v170, v171
	v_cvt_pk_fp8_f32 v209, v174, v175
	v_cvt_pk_fp8_f32 v210, v196, v197
	v_cvt_pk_fp8_f32 v211, v200, v201
	v_cvt_pk_fp8_f32 v208, v172, v173 op_sel:[0,0,1]
	v_cvt_pk_fp8_f32 v209, v176, v177 op_sel:[0,0,1]
	v_cvt_pk_fp8_f32 v210, v198, v199 op_sel:[0,0,1]
	v_cvt_pk_fp8_f32 v211, v202, v203 op_sel:[0,0,1]
	s_nop 0
	global_store_dwordx4 v28, v[208:211], s[14:15]
	ds_read_b32 v170, v8
	ds_read_b32 v171, v8 offset:512
	ds_read_b32 v172, v8 offset:1024
	ds_read_b32 v173, v8 offset:1536
	ds_read_b32 v174, v8 offset:2048
	ds_read_b32 v175, v8 offset:2560
	ds_read_b32 v176, v8 offset:3072
	ds_read_b32 v177, v8 offset:3584
	ds_read_b32 v196, v8 offset:4096
	ds_read_b32 v197, v8 offset:4608
	ds_read_b32 v198, v8 offset:5120
	ds_read_b32 v199, v8 offset:5632
	ds_read_b32 v200, v8 offset:6144
	ds_read_b32 v201, v8 offset:6656
	ds_read_b32 v202, v8 offset:7168
	ds_read_b32 v203, v8 offset:7680
	s_waitcnt lgkmcnt(0)
	v_max_f32_e32 v170, v170, v170
	v_max_f32_e32 v171, v171, v171
	v_max_f32_e32 v172, v172, v172
	v_max_f32_e32 v173, v173, v173
	v_max_f32_e32 v174, v174, v174
	v_max_f32_e32 v175, v175, v175
	v_max_f32_e32 v176, v176, v176
	v_max_f32_e32 v177, v177, v177
	v_max_f32_e32 v196, v196, v196
	v_max_f32_e32 v197, v197, v197
	v_max_f32_e32 v198, v198, v198
	v_max_f32_e32 v199, v199, v199
	v_max_f32_e32 v200, v200, v200
	v_max_f32_e32 v201, v201, v201
	v_max_f32_e32 v202, v202, v202
	v_max_f32_e32 v203, v203, v203
	v_med3_f32 v170, v170, s20, v13
	v_med3_f32 v171, v171, s20, v13
	v_med3_f32 v172, v172, s20, v13
	v_med3_f32 v173, v173, s20, v13
	v_med3_f32 v174, v174, s20, v13
	v_med3_f32 v175, v175, s20, v13
	v_med3_f32 v176, v176, s20, v13
	v_med3_f32 v177, v177, s20, v13
	v_med3_f32 v196, v196, s20, v13
	v_med3_f32 v197, v197, s20, v13
	v_med3_f32 v198, v198, s20, v13
	v_med3_f32 v199, v199, s20, v13
	v_med3_f32 v200, v200, s20, v13
	v_med3_f32 v201, v201, s20, v13
	v_med3_f32 v202, v202, s20, v13
	v_med3_f32 v203, v203, s20, v13
	v_mov_b32_e32 v208, 0
	v_mov_b32_e32 v209, 0
	v_mov_b32_e32 v210, 0
	v_mov_b32_e32 v211, 0
	v_cvt_pk_fp8_f32 v208, v170, v171
	v_cvt_pk_fp8_f32 v209, v174, v175
	v_cvt_pk_fp8_f32 v210, v196, v197
	v_cvt_pk_fp8_f32 v211, v200, v201
	v_cvt_pk_fp8_f32 v208, v172, v173 op_sel:[0,0,1]
	v_cvt_pk_fp8_f32 v209, v176, v177 op_sel:[0,0,1]
	v_cvt_pk_fp8_f32 v210, v198, v199 op_sel:[0,0,1]
	v_cvt_pk_fp8_f32 v211, v202, v203 op_sel:[0,0,1]
	s_nop 0
	global_store_dwordx4 v29, v[208:211], s[14:15]
	s_waitcnt vmcnt(32)
	v_mul_f32_e32 v132, v20, v132
	v_mul_f32_e32 v133, v20, v133
	v_mul_f32_e32 v134, v20, v134
	v_mul_f32_e32 v135, v20, v135
	ds_write_b128 v5, v[132:135]
	v_mul_f32_e32 v136, v21, v136
	v_mul_f32_e32 v137, v21, v137
	v_mul_f32_e32 v138, v21, v138
	v_mul_f32_e32 v139, v21, v139
	ds_write_b128 v5, v[136:139] offset:1024
	v_mul_f32_e32 v140, v22, v140
	v_mul_f32_e32 v141, v22, v141
	v_mul_f32_e32 v142, v22, v142
	v_mul_f32_e32 v143, v22, v143
	ds_write_b128 v5, v[140:143] offset:2048
	v_mul_f32_e32 v144, v23, v144
	v_mul_f32_e32 v145, v23, v145
	v_mul_f32_e32 v146, v23, v146
	v_mul_f32_e32 v147, v23, v147
	ds_write_b128 v5, v[144:147] offset:3072
	v_mul_f32_e32 v148, v24, v148
	v_mul_f32_e32 v149, v24, v149
	v_mul_f32_e32 v150, v24, v150
	v_mul_f32_e32 v151, v24, v151
	ds_write_b128 v5, v[148:151] offset:4096
	v_mul_f32_e32 v152, v25, v152
	v_mul_f32_e32 v153, v25, v153
	v_mul_f32_e32 v154, v25, v154
	v_mul_f32_e32 v155, v25, v155
	ds_write_b128 v5, v[152:155] offset:5120
	v_mul_f32_e32 v156, v26, v156
	v_mul_f32_e32 v157, v26, v157
	v_mul_f32_e32 v158, v26, v158
	v_mul_f32_e32 v159, v26, v159
	ds_write_b128 v5, v[156:159] offset:6144
	v_mul_f32_e32 v160, v27, v160
	v_mul_f32_e32 v161, v27, v161
	v_mul_f32_e32 v162, v27, v162
	v_mul_f32_e32 v163, v27, v163
	ds_write_b128 v5, v[160:163] offset:7168
	s_waitcnt lgkmcnt(0)
	s_barrier
; #define GAS __attribute__((address_space(1)))
; #define LAS __attribute__((address_space(3)))
; #define LDS_WAIT() asm volatile("s_waitcnt lgkmcnt(0)" ::: "memory")
;     const int pr = item >> 1, kb = 2 * (pr / nblk) + (item & 1), nb = pr % nblk, k0 = 64 * kb, n0 = 32 * nb;
;     const int nr = n0 + (lane & 31); const int sc = MAP == 1 ? src_col_in(nr) : nr;
;     float v[32];
; #pragma unroll
;     for (int i = 0; i < 32; ++i) v[i] = sc >= 0 ? W[(size_t)(k0 + 2 * i + (lane >> 5)) * Nsrc + sc] : 0.f;
; #pragma unroll
;     for (int i = 0; i < 32; ++i) { const int k = k0 + 2 * i + (lane >> 5); float x = v[i] * wscale; if (KS) x *= (k < ksplit ? ksA[k] : ksB[k - ksplit]); scr[(2 * i + (lane >> 5)) * 33 + (lane & 31)] = x; }
;     LDS_WAIT(); asm volatile("" ::: "memory");
;     const int c = lane & 7;
; #pragma unroll
;     for (int j = 0; j < 4; ++j) { const int n = (lane >> 3) + 8 * j; const LAS float* s = scr + (8 * c) * 33 + n;
;         const unsigned long long o = (unsigned long long)pg8::pk4_fp8(s[0 * 33], s[1 * 33], s[2 * 33], s[3 * 33]) | ((unsigned long long)pg8::pk4_fp8(s[4 * 33], s[5 * 33], s[6 * 33], s[7 * 33]) << 32);
;         *(GAS unsigned long long*)(WT + (size_t)(n0 + n) * K + k0 + 8 * c) = o; }
;     LDS_WAIT(); asm volatile("" ::: "memory");
; __global__ void __launch_bounds__(NWAVES * 64, 2) hybrid_fwd(Args args) {
;     ...
;             if (r < I_O) { if (l >= WO_F8_FROM) p0_transpose_item_f8<true>(args.in[13] + (size_t)l * DM * DM, DM, DM, DM / 32, (unsigned char*)(ws + WS_WO + l * SZ_WO), 64.f, args.in[6] + l * 2048, args.in[12] + l * 2048, 2048, scr, r, lane);
;                 else p0_transpose_item<0, true>(args.in[13] + (size_t)l * DM * DM, DM, DM, DM / 32, (bf16*)(ws + WS_WO + l * SZ_WO), args.in[6] + l * 2048, args.in[12] + l * 2048, 2048, scr, r, lane); continue; } r -= I_O;
;             if (r < I_UP) { p0_transpose_item_f8<true>(args.in[15] + (size_t)l * DM * FF, DM, FF, FF / 32, (unsigned char*)(ws + WS_WUP + l * SZ_WUP), WUP8_SCALE, args.in[14] + l * DM, args.in[14] + l * DM, DM, scr, r, lane); continue; } r -= I_UP;
;             p0_transpose_item_f8<false>(args.in[16] + (size_t)l * FF * DM, FF, DM, DM / 32, (unsigned char*)(ws + WS_WDN + l * SZ_WDN), 128.f, args.in[16], args.in[16], 0, scr, r, lane);
	s_add_i32 s19, s39, 24
	s_min_u32 s19, s19, 31
	s_lshl_b32 s19, s19, 9
	s_add_u32 s12, s22, s19
	s_addc_u32 s13, s23, 0
	global_load_dwordx4 v[132:135], v10, s[12:13]
	s_add_u32 s12, s12, 0x8000
	s_addc_u32 s13, s13, 0
	global_load_dwordx4 v[136:139], v10, s[12:13]
	s_add_u32 s12, s12, 0x8000
	s_addc_u32 s13, s13, 0
	global_load_dwordx4 v[140:143], v10, s[12:13]
	s_add_u32 s12, s12, 0x8000
	s_addc_u32 s13, s13, 0
	global_load_dwordx4 v[144:147], v10, s[12:13]
	s_add_u32 s12, s12, 0x8000
	s_addc_u32 s13, s13, 0
	global_load_dwordx4 v[148:151], v10, s[12:13]
	s_add_u32 s12, s12, 0x8000
	s_addc_u32 s13, s13, 0
	global_load_dwordx4 v[152:155], v10, s[12:13]
	s_add_u32 s12, s12, 0x8000
	s_addc_u32 s13, s13, 0
	global_load_dwordx4 v[156:159], v10, s[12:13]
	s_add_u32 s12, s12, 0x8000
	s_addc_u32 s13, s13, 0
	global_load_dwordx4 v[160:163], v10, s[12:13]
	s_add_i32 s19, s39, 12
	s_min_u32 s19, s19, 31
	s_lshl_b32 s19, s19, 19
	s_add_u32 s14, s50, s19
	s_addc_u32 s15, s51, 0
	ds_read_b32 v170, v7
	ds_read_b32 v171, v7 offset:512
	ds_read_b32 v172, v7 offset:1024
	ds_read_b32 v173, v7 offset:1536
	ds_read_b32 v174, v7 offset:2048
	ds_read_b32 v175, v7 offset:2560
	ds_read_b32 v176, v7 offset:3072
	ds_read_b32 v177, v7 offset:3584
	ds_read_b32 v196, v7 offset:4096
	ds_read_b32 v197, v7 offset:4608
	ds_read_b32 v198, v7 offset:5120
	ds_read_b32 v199, v7 offset:5632
	ds_read_b32 v200, v7 offset:6144
	ds_read_b32 v201, v7 offset:6656
	ds_read_b32 v202, v7 offset:7168
	ds_read_b32 v203, v7 offset:7680
	s_waitcnt lgkmcnt(0)
	v_max_f32_e32 v170, v170, v170
	v_max_f32_e32 v171, v171, v171
	v_max_f32_e32 v172, v172, v172
	v_max_f32_e32 v173, v173, v173
	v_max_f32_e32 v174, v174, v174
	v_max_f32_e32 v175, v175, v175
	v_max_f32_e32 v176, v176, v176
	v_max_f32_e32 v177, v177, v177
	v_max_f32_e32 v196, v196, v196
	v_max_f32_e32 v197, v197, v197
	v_max_f32_e32 v198, v198, v198
	v_max_f32_e32 v199, v199, v199
	v_max_f32_e32 v200, v200, v200
	v_max_f32_e32 v201, v201, v201
	v_max_f32_e32 v202, v202, v202
	v_max_f32_e32 v203, v203, v203
	v_med3_f32 v170, v170, s20, v13
	v_med3_f32 v171, v171, s20, v13
	v_med3_f32 v172, v172, s20, v13
	v_med3_f32 v173, v173, s20, v13
	v_med3_f32 v174, v174, s20, v13
	v_med3_f32 v175, v175, s20, v13
	v_med3_f32 v176, v176, s20, v13
	v_med3_f32 v177, v177, s20, v13
	v_med3_f32 v196, v196, s20, v13
	v_med3_f32 v197, v197, s20, v13
	v_med3_f32 v198, v198, s20, v13
	v_med3_f32 v199, v199, s20, v13
	v_med3_f32 v200, v200, s20, v13
	v_med3_f32 v201, v201, s20, v13
	v_med3_f32 v202, v202, s20, v13
	v_med3_f32 v203, v203, s20, v13
	v_mov_b32_e32 v208, 0
	v_mov_b32_e32 v209, 0
	v_mov_b32_e32 v210, 0
	v_mov_b32_e32 v211, 0
	v_cvt_pk_fp8_f32 v208, v170, v171
	v_cvt_pk_fp8_f32 v209, v174, v175
	v_cvt_pk_fp8_f32 v210, v196, v197
	v_cvt_pk_fp8_f32 v211, v200, v201
	v_cvt_pk_fp8_f32 v208, v172, v173 op_sel:[0,0,1]
	v_cvt_pk_fp8_f32 v209, v176, v177 op_sel:[0,0,1]
	v_cvt_pk_fp8_f32 v210, v198, v199 op_sel:[0,0,1]
	v_cvt_pk_fp8_f32 v211, v202, v203 op_sel:[0,0,1]
	s_nop 0
	global_store_dwordx4 v28, v[208:211], s[14:15]
	ds_read_b32 v170, v9
	ds_read_b32 v171, v9 offset:512
	ds_read_b32 v172, v9 offset:1024
	ds_read_b32 v173, v9 offset:1536
	ds_read_b32 v174, v9 offset:2048
	ds_read_b32 v175, v9 offset:2560
	ds_read_b32 v176, v9 offset:3072
	ds_read_b32 v177, v9 offset:3584
	ds_read_b32 v196, v9 offset:4096
	ds_read_b32 v197, v9 offset:4608
	ds_read_b32 v198, v9 offset:5120
	ds_read_b32 v199, v9 offset:5632
	ds_read_b32 v200, v9 offset:6144
	ds_read_b32 v201, v9 offset:6656
	ds_read_b32 v202, v9 offset:7168
	ds_read_b32 v203, v9 offset:7680
	s_waitcnt lgkmcnt(0)
	v_max_f32_e32 v170, v170, v170
	v_max_f32_e32 v171, v171, v171
	v_max_f32_e32 v172, v172, v172
	v_max_f32_e32 v173, v173, v173
	v_max_f32_e32 v174, v174, v174
	v_max_f32_e32 v175, v175, v175
	v_max_f32_e32 v176, v176, v176
	v_max_f32_e32 v177, v177, v177
	v_max_f32_e32 v196, v196, v196
	v_max_f32_e32 v197, v197, v197
	v_max_f32_e32 v198, v198, v198
	v_max_f32_e32 v199, v199, v199
	v_max_f32_e32 v200, v200, v200
	v_max_f32_e32 v201, v201, v201
	v_max_f32_e32 v202, v202, v202
	v_max_f32_e32 v203, v203, v203
	v_med3_f32 v170, v170, s20, v13
	v_med3_f32 v171, v171, s20, v13
	v_med3_f32 v172, v172, s20, v13
	v_med3_f32 v173, v173, s20, v13
	v_med3_f32 v174, v174, s20, v13
	v_med3_f32 v175, v175, s20, v13
	v_med3_f32 v176, v176, s20, v13
	v_med3_f32 v177, v177, s20, v13
	v_med3_f32 v196, v196, s20, v13
	v_med3_f32 v197, v197, s20, v13
	v_med3_f32 v198, v198, s20, v13
	v_med3_f32 v199, v199, s20, v13
	v_med3_f32 v200, v200, s20, v13
	v_med3_f32 v201, v201, s20, v13
	v_med3_f32 v202, v202, s20, v13
	v_med3_f32 v203, v203, s20, v13
	v_mov_b32_e32 v208, 0
	v_mov_b32_e32 v209, 0
	v_mov_b32_e32 v210, 0
	v_mov_b32_e32 v211, 0
	v_cvt_pk_fp8_f32 v208, v170, v171
	v_cvt_pk_fp8_f32 v209, v174, v175
	v_cvt_pk_fp8_f32 v210, v196, v197
	v_cvt_pk_fp8_f32 v211, v200, v201
	v_cvt_pk_fp8_f32 v208, v172, v173 op_sel:[0,0,1]
	v_cvt_pk_fp8_f32 v209, v176, v177 op_sel:[0,0,1]
	v_cvt_pk_fp8_f32 v210, v198, v199 op_sel:[0,0,1]
	v_cvt_pk_fp8_f32 v211, v202, v203 op_sel:[0,0,1]
	s_nop 0
	global_store_dwordx4 v29, v[208:211], s[14:15]
	s_waitcnt vmcnt(32)
	v_mul_f32_e32 v36, v20, v36
	v_mul_f32_e32 v37, v20, v37
	v_mul_f32_e32 v38, v20, v38
	v_mul_f32_e32 v39, v20, v39
	ds_write_b128 v4, v[36:39]
	v_mul_f32_e32 v40, v21, v40
	v_mul_f32_e32 v41, v21, v41
	v_mul_f32_e32 v42, v21, v42
	v_mul_f32_e32 v43, v21, v43
	ds_write_b128 v4, v[40:43] offset:1024
	v_mul_f32_e32 v44, v22, v44
	v_mul_f32_e32 v45, v22, v45
	v_mul_f32_e32 v46, v22, v46
	v_mul_f32_e32 v47, v22, v47
	ds_write_b128 v4, v[44:47] offset:2048
	v_mul_f32_e32 v48, v23, v48
	v_mul_f32_e32 v49, v23, v49
	v_mul_f32_e32 v50, v23, v50
	v_mul_f32_e32 v51, v23, v51
	ds_write_b128 v4, v[48:51] offset:3072
	v_mul_f32_e32 v52, v24, v52
	v_mul_f32_e32 v53, v24, v53
	v_mul_f32_e32 v54, v24, v54
	v_mul_f32_e32 v55, v24, v55
	ds_write_b128 v4, v[52:55] offset:4096
	v_mul_f32_e32 v56, v25, v56
	v_mul_f32_e32 v57, v25, v57
	v_mul_f32_e32 v58, v25, v58
	v_mul_f32_e32 v59, v25, v59
	ds_write_b128 v4, v[56:59] offset:5120
	v_mul_f32_e32 v60, v26, v60
	v_mul_f32_e32 v61, v26, v61
	v_mul_f32_e32 v62, v26, v62
	v_mul_f32_e32 v63, v26, v63
	ds_write_b128 v4, v[60:63] offset:6144
	v_mul_f32_e32 v64, v27, v64
	v_mul_f32_e32 v65, v27, v65
	v_mul_f32_e32 v66, v27, v66
	v_mul_f32_e32 v67, v27, v67
	ds_write_b128 v4, v[64:67] offset:7168
	s_waitcnt lgkmcnt(0)
	s_barrier
; #define GAS __attribute__((address_space(1)))
; #define LAS __attribute__((address_space(3)))
; #define LDS_WAIT() asm volatile("s_waitcnt lgkmcnt(0)" ::: "memory")
;     const int pr = item >> 1, kb = 2 * (pr / nblk) + (item & 1), nb = pr % nblk, k0 = 64 * kb, n0 = 32 * nb;
;     const int nr = n0 + (lane & 31); const int sc = MAP == 1 ? src_col_in(nr) : nr;
;     float v[32];
; #pragma unroll
;     for (int i = 0; i < 32; ++i) v[i] = sc >= 0 ? W[(size_t)(k0 + 2 * i + (lane >> 5)) * Nsrc + sc] : 0.f;
; #pragma unroll
;     for (int i = 0; i < 32; ++i) { const int k = k0 + 2 * i + (lane >> 5); float x = v[i] * wscale; if (KS) x *= (k < ksplit ? ksA[k] : ksB[k - ksplit]); scr[(2 * i + (lane >> 5)) * 33 + (lane & 31)] = x; }
;     LDS_WAIT(); asm volatile("" ::: "memory");
;     const int c = lane & 7;
; #pragma unroll
;     for (int j = 0; j < 4; ++j) { const int n = (lane >> 3) + 8 * j; const LAS float* s = scr + (8 * c) * 33 + n;
;         const unsigned long long o = (unsigned long long)pg8::pk4_fp8(s[0 * 33], s[1 * 33], s[2 * 33], s[3 * 33]) | ((unsigned long long)pg8::pk4_fp8(s[4 * 33], s[5 * 33], s[6 * 33], s[7 * 33]) << 32);
;         *(GAS unsigned long long*)(WT + (size_t)(n0 + n) * K + k0 + 8 * c) = o; }
;     LDS_WAIT(); asm volatile("" ::: "memory");
; __global__ void __launch_bounds__(NWAVES * 64, 2) hybrid_fwd(Args args) {
;     ...
;             if (r < I_O) { if (l >= WO_F8_FROM) p0_transpose_item_f8<true>(args.in[13] + (size_t)l * DM * DM, DM, DM, DM / 32, (unsigned char*)(ws + WS_WO + l * SZ_WO), 64.f, args.in[6] + l * 2048, args.in[12] + l * 2048, 2048, scr, r, lane);
;                 else p0_transpose_item<0, true>(args.in[13] + (size_t)l * DM * DM, DM, DM, DM / 32, (bf16*)(ws + WS_WO + l * SZ_WO), args.in[6] + l * 2048, args.in[12] + l * 2048, 2048, scr, r, lane); continue; } r -= I_O;
;             if (r < I_UP) { p0_transpose_item_f8<true>(args.in[15] + (size_t)l * DM * FF, DM, FF, FF / 32, (unsigned char*)(ws + WS_WUP + l * SZ_WUP), WUP8_SCALE, args.in[14] + l * DM, args.in[14] + l * DM, DM, scr, r, lane); continue; } r -= I_UP;
;             p0_transpose_item_f8<false>(args.in[16] + (size_t)l * FF * DM, FF, DM, DM / 32, (unsigned char*)(ws + WS_WDN + l * SZ_WDN), 128.f, args.in[16], args.in[16], 0, scr, r, lane);
	s_add_i32 s19, s39, 27
	s_min_u32 s19, s19, 31
	s_lshl_b32 s19, s19, 9
	s_add_u32 s12, s22, s19
	s_addc_u32 s13, s23, 0
	global_load_dwordx4 v[36:39], v10, s[12:13]
	s_add_u32 s12, s12, 0x8000
	s_addc_u32 s13, s13, 0
	global_load_dwordx4 v[40:43], v10, s[12:13]
	s_add_u32 s12, s12, 0x8000
	s_addc_u32 s13, s13, 0
	global_load_dwordx4 v[44:47], v10, s[12:13]
	s_add_u32 s12, s12, 0x8000
	s_addc_u32 s13, s13, 0
	global_load_dwordx4 v[48:51], v10, s[12:13]
	s_add_u32 s12, s12, 0x8000
	s_addc_u32 s13, s13, 0
	global_load_dwordx4 v[52:55], v10, s[12:13]
	s_add_u32 s12, s12, 0x8000
	s_addc_u32 s13, s13, 0
	global_load_dwordx4 v[56:59], v10, s[12:13]
	s_add_u32 s12, s12, 0x8000
	s_addc_u32 s13, s13, 0
	global_load_dwordx4 v[60:63], v10, s[12:13]
	s_add_u32 s12, s12, 0x8000
	s_addc_u32 s13, s13, 0
	global_load_dwordx4 v[64:67], v10, s[12:13]
	s_add_i32 s19, s39, 15
	s_min_u32 s19, s19, 31
	s_lshl_b32 s19, s19, 19
	s_add_u32 s14, s50, s19
	s_addc_u32 s15, s51, 0
	ds_read_b32 v170, v6
	ds_read_b32 v171, v6 offset:512
	ds_read_b32 v172, v6 offset:1024
	ds_read_b32 v173, v6 offset:1536
	ds_read_b32 v174, v6 offset:2048
	ds_read_b32 v175, v6 offset:2560
	ds_read_b32 v176, v6 offset:3072
	ds_read_b32 v177, v6 offset:3584
	ds_read_b32 v196, v6 offset:4096
	ds_read_b32 v197, v6 offset:4608
	ds_read_b32 v198, v6 offset:5120
	ds_read_b32 v199, v6 offset:5632
	ds_read_b32 v200, v6 offset:6144
	ds_read_b32 v201, v6 offset:6656
	ds_read_b32 v202, v6 offset:7168
	ds_read_b32 v203, v6 offset:7680
	s_waitcnt lgkmcnt(0)
	v_max_f32_e32 v170, v170, v170
	v_max_f32_e32 v171, v171, v171
	v_max_f32_e32 v172, v172, v172
	v_max_f32_e32 v173, v173, v173
	v_max_f32_e32 v174, v174, v174
	v_max_f32_e32 v175, v175, v175
	v_max_f32_e32 v176, v176, v176
	v_max_f32_e32 v177, v177, v177
	v_max_f32_e32 v196, v196, v196
	v_max_f32_e32 v197, v197, v197
	v_max_f32_e32 v198, v198, v198
	v_max_f32_e32 v199, v199, v199
	v_max_f32_e32 v200, v200, v200
	v_max_f32_e32 v201, v201, v201
	v_max_f32_e32 v202, v202, v202
	v_max_f32_e32 v203, v203, v203
	v_med3_f32 v170, v170, s20, v13
	v_med3_f32 v171, v171, s20, v13
	v_med3_f32 v172, v172, s20, v13
	v_med3_f32 v173, v173, s20, v13
	v_med3_f32 v174, v174, s20, v13
	v_med3_f32 v175, v175, s20, v13
	v_med3_f32 v176, v176, s20, v13
	v_med3_f32 v177, v177, s20, v13
	v_med3_f32 v196, v196, s20, v13
	v_med3_f32 v197, v197, s20, v13
	v_med3_f32 v198, v198, s20, v13
	v_med3_f32 v199, v199, s20, v13
	v_med3_f32 v200, v200, s20, v13
	v_med3_f32 v201, v201, s20, v13
	v_med3_f32 v202, v202, s20, v13
	v_med3_f32 v203, v203, s20, v13
	v_mov_b32_e32 v208, 0
	v_mov_b32_e32 v209, 0
	v_mov_b32_e32 v210, 0
	v_mov_b32_e32 v211, 0
	v_cvt_pk_fp8_f32 v208, v170, v171
	v_cvt_pk_fp8_f32 v209, v174, v175
	v_cvt_pk_fp8_f32 v210, v196, v197
	v_cvt_pk_fp8_f32 v211, v200, v201
	v_cvt_pk_fp8_f32 v208, v172, v173 op_sel:[0,0,1]
	v_cvt_pk_fp8_f32 v209, v176, v177 op_sel:[0,0,1]
	v_cvt_pk_fp8_f32 v210, v198, v199 op_sel:[0,0,1]
	v_cvt_pk_fp8_f32 v211, v202, v203 op_sel:[0,0,1]
	s_nop 0
	global_store_dwordx4 v28, v[208:211], s[14:15]
	ds_read_b32 v170, v8
	ds_read_b32 v171, v8 offset:512
	ds_read_b32 v172, v8 offset:1024
	ds_read_b32 v173, v8 offset:1536
	ds_read_b32 v174, v8 offset:2048
	ds_read_b32 v175, v8 offset:2560
	ds_read_b32 v176, v8 offset:3072
	ds_read_b32 v177, v8 offset:3584
	ds_read_b32 v196, v8 offset:4096
	ds_read_b32 v197, v8 offset:4608
	ds_read_b32 v198, v8 offset:5120
	ds_read_b32 v199, v8 offset:5632
	ds_read_b32 v200, v8 offset:6144
	ds_read_b32 v201, v8 offset:6656
	ds_read_b32 v202, v8 offset:7168
	ds_read_b32 v203, v8 offset:7680
	s_waitcnt lgkmcnt(0)
	v_max_f32_e32 v170, v170, v170
	v_max_f32_e32 v171, v171, v171
	v_max_f32_e32 v172, v172, v172
	v_max_f32_e32 v173, v173, v173
	v_max_f32_e32 v174, v174, v174
	v_max_f32_e32 v175, v175, v175
	v_max_f32_e32 v176, v176, v176
	v_max_f32_e32 v177, v177, v177
	v_max_f32_e32 v196, v196, v196
	v_max_f32_e32 v197, v197, v197
	v_max_f32_e32 v198, v198, v198
	v_max_f32_e32 v199, v199, v199
	v_max_f32_e32 v200, v200, v200
	v_max_f32_e32 v201, v201, v201
	v_max_f32_e32 v202, v202, v202
	v_max_f32_e32 v203, v203, v203
	v_med3_f32 v170, v170, s20, v13
	v_med3_f32 v171, v171, s20, v13
	v_med3_f32 v172, v172, s20, v13
	v_med3_f32 v173, v173, s20, v13
	v_med3_f32 v174, v174, s20, v13
	v_med3_f32 v175, v175, s20, v13
	v_med3_f32 v176, v176, s20, v13
	v_med3_f32 v177, v177, s20, v13
	v_med3_f32 v196, v196, s20, v13
	v_med3_f32 v197, v197, s20, v13
	v_med3_f32 v198, v198, s20, v13
	v_med3_f32 v199, v199, s20, v13
	v_med3_f32 v200, v200, s20, v13
	v_med3_f32 v201, v201, s20, v13
	v_med3_f32 v202, v202, s20, v13
	v_med3_f32 v203, v203, s20, v13
	v_mov_b32_e32 v208, 0
	v_mov_b32_e32 v209, 0
	v_mov_b32_e32 v210, 0
	v_mov_b32_e32 v211, 0
	v_cvt_pk_fp8_f32 v208, v170, v171
	v_cvt_pk_fp8_f32 v209, v174, v175
	v_cvt_pk_fp8_f32 v210, v196, v197
	v_cvt_pk_fp8_f32 v211, v200, v201
	v_cvt_pk_fp8_f32 v208, v172, v173 op_sel:[0,0,1]
	v_cvt_pk_fp8_f32 v209, v176, v177 op_sel:[0,0,1]
	v_cvt_pk_fp8_f32 v210, v198, v199 op_sel:[0,0,1]
	v_cvt_pk_fp8_f32 v211, v202, v203 op_sel:[0,0,1]
	s_nop 0
	global_store_dwordx4 v29, v[208:211], s[14:15]
	s_waitcnt vmcnt(32)
	v_mul_f32_e32 v68, v20, v68
	v_mul_f32_e32 v69, v20, v69
	v_mul_f32_e32 v70, v20, v70
	v_mul_f32_e32 v71, v20, v71
	ds_write_b128 v5, v[68:71]
	v_mul_f32_e32 v72, v21, v72
	v_mul_f32_e32 v73, v21, v73
	v_mul_f32_e32 v74, v21, v74
	v_mul_f32_e32 v75, v21, v75
	ds_write_b128 v5, v[72:75] offset:1024
	v_mul_f32_e32 v76, v22, v76
	v_mul_f32_e32 v77, v22, v77
	v_mul_f32_e32 v78, v22, v78
	v_mul_f32_e32 v79, v22, v79
	ds_write_b128 v5, v[76:79] offset:2048
	v_mul_f32_e32 v80, v23, v80
	v_mul_f32_e32 v81, v23, v81
	v_mul_f32_e32 v82, v23, v82
	v_mul_f32_e32 v83, v23, v83
	ds_write_b128 v5, v[80:83] offset:3072
	v_mul_f32_e32 v84, v24, v84
	v_mul_f32_e32 v85, v24, v85
	v_mul_f32_e32 v86, v24, v86
	v_mul_f32_e32 v87, v24, v87
	ds_write_b128 v5, v[84:87] offset:4096
	v_mul_f32_e32 v88, v25, v88
	v_mul_f32_e32 v89, v25, v89
	v_mul_f32_e32 v90, v25, v90
	v_mul_f32_e32 v91, v25, v91
	ds_write_b128 v5, v[88:91] offset:5120
	v_mul_f32_e32 v92, v26, v92
	v_mul_f32_e32 v93, v26, v93
	v_mul_f32_e32 v94, v26, v94
	v_mul_f32_e32 v95, v26, v95
	ds_write_b128 v5, v[92:95] offset:6144
	v_mul_f32_e32 v96, v27, v96
	v_mul_f32_e32 v97, v27, v97
	v_mul_f32_e32 v98, v27, v98
	v_mul_f32_e32 v99, v27, v99
	ds_write_b128 v5, v[96:99] offset:7168
	s_waitcnt lgkmcnt(0)
	s_barrier
; #define GAS __attribute__((address_space(1)))
; #define LAS __attribute__((address_space(3)))
; #define LDS_WAIT() asm volatile("s_waitcnt lgkmcnt(0)" ::: "memory")
;     const int pr = item >> 1, kb = 2 * (pr / nblk) + (item & 1), nb = pr % nblk, k0 = 64 * kb, n0 = 32 * nb;
;     const int nr = n0 + (lane & 31); const int sc = MAP == 1 ? src_col_in(nr) : nr;
;     float v[32];
; #pragma unroll
;     for (int i = 0; i < 32; ++i) v[i] = sc >= 0 ? W[(size_t)(k0 + 2 * i + (lane >> 5)) * Nsrc + sc] : 0.f;
; #pragma unroll
;     for (int i = 0; i < 32; ++i) { const int k = k0 + 2 * i + (lane >> 5); float x = v[i] * wscale; if (KS) x *= (k < ksplit ? ksA[k] : ksB[k - ksplit]); scr[(2 * i + (lane >> 5)) * 33 + (lane & 31)] = x; }
;     LDS_WAIT(); asm volatile("" ::: "memory");
;     const int c = lane & 7;
; #pragma unroll
;     for (int j = 0; j < 4; ++j) { const int n = (lane >> 3) + 8 * j; const LAS float* s = scr + (8 * c) * 33 + n;
;         const unsigned long long o = (unsigned long long)pg8::pk4_fp8(s[0 * 33], s[1 * 33], s[2 * 33], s[3 * 33]) | ((unsigned long long)pg8::pk4_fp8(s[4 * 33], s[5 * 33], s[6 * 33], s[7 * 33]) << 32);
;         *(GAS unsigned long long*)(WT + (size_t)(n0 + n) * K + k0 + 8 * c) = o; }
;     LDS_WAIT(); asm volatile("" ::: "memory");
; __global__ void __launch_bounds__(NWAVES * 64, 2) hybrid_fwd(Args args) {
;     ...
;             if (r < I_O) { if (l >= WO_F8_FROM) p0_transpose_item_f8<true>(args.in[13] + (size_t)l * DM * DM, DM, DM, DM / 32, (unsigned char*)(ws + WS_WO + l * SZ_WO), 64.f, args.in[6] + l * 2048, args.in[12] + l * 2048, 2048, scr, r, lane);
;                 else p0_transpose_item<0, true>(args.in[13] + (size_t)l * DM * DM, DM, DM, DM / 32, (bf16*)(ws + WS_WO + l * SZ_WO), args.in[6] + l * 2048, args.in[12] + l * 2048, 2048, scr, r, lane); continue; } r -= I_O;
;             if (r < I_UP) { p0_transpose_item_f8<true>(args.in[15] + (size_t)l * DM * FF, DM, FF, FF / 32, (unsigned char*)(ws + WS_WUP + l * SZ_WUP), WUP8_SCALE, args.in[14] + l * DM, args.in[14] + l * DM, DM, scr, r, lane); continue; } r -= I_UP;
;             p0_transpose_item_f8<false>(args.in[16] + (size_t)l * FF * DM, FF, DM, DM / 32, (unsigned char*)(ws + WS_WDN + l * SZ_WDN), 128.f, args.in[16], args.in[16], 0, scr, r, lane);
	s_add_i32 s19, s39, 30
	s_min_u32 s19, s19, 31
	s_lshl_b32 s19, s19, 9
	s_add_u32 s12, s22, s19
	s_addc_u32 s13, s23, 0
	global_load_dwordx4 v[68:71], v10, s[12:13]
	s_add_u32 s12, s12, 0x8000
	s_addc_u32 s13, s13, 0
	global_load_dwordx4 v[72:75], v10, s[12:13]
	s_add_u32 s12, s12, 0x8000
	s_addc_u32 s13, s13, 0
	global_load_dwordx4 v[76:79], v10, s[12:13]
	s_add_u32 s12, s12, 0x8000
	s_addc_u32 s13, s13, 0
	global_load_dwordx4 v[80:83], v10, s[12:13]
	s_add_u32 s12, s12, 0x8000
	s_addc_u32 s13, s13, 0
	global_load_dwordx4 v[84:87], v10, s[12:13]
	s_add_u32 s12, s12, 0x8000
	s_addc_u32 s13, s13, 0
	global_load_dwordx4 v[88:91], v10, s[12:13]
	s_add_u32 s12, s12, 0x8000
	s_addc_u32 s13, s13, 0
	global_load_dwordx4 v[92:95], v10, s[12:13]
	s_add_u32 s12, s12, 0x8000
	s_addc_u32 s13, s13, 0
	global_load_dwordx4 v[96:99], v10, s[12:13]
	s_add_i32 s19, s39, 18
	s_min_u32 s19, s19, 31
	s_lshl_b32 s19, s19, 19
	s_add_u32 s14, s50, s19
	s_addc_u32 s15, s51, 0
	ds_read_b32 v170, v7
	ds_read_b32 v171, v7 offset:512
	ds_read_b32 v172, v7 offset:1024
	ds_read_b32 v173, v7 offset:1536
	ds_read_b32 v174, v7 offset:2048
	ds_read_b32 v175, v7 offset:2560
	ds_read_b32 v176, v7 offset:3072
	ds_read_b32 v177, v7 offset:3584
	ds_read_b32 v196, v7 offset:4096
	ds_read_b32 v197, v7 offset:4608
	ds_read_b32 v198, v7 offset:5120
	ds_read_b32 v199, v7 offset:5632
	ds_read_b32 v200, v7 offset:6144
	ds_read_b32 v201, v7 offset:6656
	ds_read_b32 v202, v7 offset:7168
	ds_read_b32 v203, v7 offset:7680
	s_waitcnt lgkmcnt(0)
	v_max_f32_e32 v170, v170, v170
	v_max_f32_e32 v171, v171, v171
	v_max_f32_e32 v172, v172, v172
	v_max_f32_e32 v173, v173, v173
	v_max_f32_e32 v174, v174, v174
	v_max_f32_e32 v175, v175, v175
	v_max_f32_e32 v176, v176, v176
	v_max_f32_e32 v177, v177, v177
	v_max_f32_e32 v196, v196, v196
	v_max_f32_e32 v197, v197, v197
	v_max_f32_e32 v198, v198, v198
	v_max_f32_e32 v199, v199, v199
	v_max_f32_e32 v200, v200, v200
	v_max_f32_e32 v201, v201, v201
	v_max_f32_e32 v202, v202, v202
	v_max_f32_e32 v203, v203, v203
	v_med3_f32 v170, v170, s20, v13
	v_med3_f32 v171, v171, s20, v13
	v_med3_f32 v172, v172, s20, v13
	v_med3_f32 v173, v173, s20, v13
	v_med3_f32 v174, v174, s20, v13
	v_med3_f32 v175, v175, s20, v13
	v_med3_f32 v176, v176, s20, v13
	v_med3_f32 v177, v177, s20, v13
	v_med3_f32 v196, v196, s20, v13
	v_med3_f32 v197, v197, s20, v13
	v_med3_f32 v198, v198, s20, v13
	v_med3_f32 v199, v199, s20, v13
	v_med3_f32 v200, v200, s20, v13
	v_med3_f32 v201, v201, s20, v13
	v_med3_f32 v202, v202, s20, v13
	v_med3_f32 v203, v203, s20, v13
	v_mov_b32_e32 v208, 0
	v_mov_b32_e32 v209, 0
	v_mov_b32_e32 v210, 0
	v_mov_b32_e32 v211, 0
	v_cvt_pk_fp8_f32 v208, v170, v171
	v_cvt_pk_fp8_f32 v209, v174, v175
	v_cvt_pk_fp8_f32 v210, v196, v197
	v_cvt_pk_fp8_f32 v211, v200, v201
	v_cvt_pk_fp8_f32 v208, v172, v173 op_sel:[0,0,1]
	v_cvt_pk_fp8_f32 v209, v176, v177 op_sel:[0,0,1]
	v_cvt_pk_fp8_f32 v210, v198, v199 op_sel:[0,0,1]
	v_cvt_pk_fp8_f32 v211, v202, v203 op_sel:[0,0,1]
	s_nop 0
	global_store_dwordx4 v28, v[208:211], s[14:15]
	ds_read_b32 v170, v9
	ds_read_b32 v171, v9 offset:512
	ds_read_b32 v172, v9 offset:1024
	ds_read_b32 v173, v9 offset:1536
	ds_read_b32 v174, v9 offset:2048
	ds_read_b32 v175, v9 offset:2560
	ds_read_b32 v176, v9 offset:3072
	ds_read_b32 v177, v9 offset:3584
	ds_read_b32 v196, v9 offset:4096
	ds_read_b32 v197, v9 offset:4608
	ds_read_b32 v198, v9 offset:5120
	ds_read_b32 v199, v9 offset:5632
	ds_read_b32 v200, v9 offset:6144
	ds_read_b32 v201, v9 offset:6656
	ds_read_b32 v202, v9 offset:7168
	ds_read_b32 v203, v9 offset:7680
	s_waitcnt lgkmcnt(0)
	v_max_f32_e32 v170, v170, v170
	v_max_f32_e32 v171, v171, v171
	v_max_f32_e32 v172, v172, v172
	v_max_f32_e32 v173, v173, v173
	v_max_f32_e32 v174, v174, v174
	v_max_f32_e32 v175, v175, v175
	v_max_f32_e32 v176, v176, v176
	v_max_f32_e32 v177, v177, v177
	v_max_f32_e32 v196, v196, v196
	v_max_f32_e32 v197, v197, v197
	v_max_f32_e32 v198, v198, v198
	v_max_f32_e32 v199, v199, v199
	v_max_f32_e32 v200, v200, v200
	v_max_f32_e32 v201, v201, v201
	v_max_f32_e32 v202, v202, v202
	v_max_f32_e32 v203, v203, v203
	v_med3_f32 v170, v170, s20, v13
	v_med3_f32 v171, v171, s20, v13
	v_med3_f32 v172, v172, s20, v13
	v_med3_f32 v173, v173, s20, v13
	v_med3_f32 v174, v174, s20, v13
	v_med3_f32 v175, v175, s20, v13
	v_med3_f32 v176, v176, s20, v13
	v_med3_f32 v177, v177, s20, v13
	v_med3_f32 v196, v196, s20, v13
	v_med3_f32 v197, v197, s20, v13
	v_med3_f32 v198, v198, s20, v13
	v_med3_f32 v199, v199, s20, v13
	v_med3_f32 v200, v200, s20, v13
	v_med3_f32 v201, v201, s20, v13
	v_med3_f32 v202, v202, s20, v13
	v_med3_f32 v203, v203, s20, v13
	v_mov_b32_e32 v208, 0
	v_mov_b32_e32 v209, 0
	v_mov_b32_e32 v210, 0
	v_mov_b32_e32 v211, 0
	v_cvt_pk_fp8_f32 v208, v170, v171
	v_cvt_pk_fp8_f32 v209, v174, v175
	v_cvt_pk_fp8_f32 v210, v196, v197
	v_cvt_pk_fp8_f32 v211, v200, v201
	v_cvt_pk_fp8_f32 v208, v172, v173 op_sel:[0,0,1]
	v_cvt_pk_fp8_f32 v209, v176, v177 op_sel:[0,0,1]
	v_cvt_pk_fp8_f32 v210, v198, v199 op_sel:[0,0,1]
	v_cvt_pk_fp8_f32 v211, v202, v203 op_sel:[0,0,1]
	s_nop 0
	global_store_dwordx4 v29, v[208:211], s[14:15]
	s_waitcnt vmcnt(32)
	v_mul_f32_e32 v100, v20, v100
	v_mul_f32_e32 v101, v20, v101
	v_mul_f32_e32 v102, v20, v102
	v_mul_f32_e32 v103, v20, v103
	ds_write_b128 v4, v[100:103]
	v_mul_f32_e32 v104, v21, v104
	v_mul_f32_e32 v105, v21, v105
	v_mul_f32_e32 v106, v21, v106
	v_mul_f32_e32 v107, v21, v107
	ds_write_b128 v4, v[104:107] offset:1024
	v_mul_f32_e32 v108, v22, v108
	v_mul_f32_e32 v109, v22, v109
	v_mul_f32_e32 v110, v22, v110
	v_mul_f32_e32 v111, v22, v111
	ds_write_b128 v4, v[108:111] offset:2048
	v_mul_f32_e32 v112, v23, v112
	v_mul_f32_e32 v113, v23, v113
	v_mul_f32_e32 v114, v23, v114
	v_mul_f32_e32 v115, v23, v115
	ds_write_b128 v4, v[112:115] offset:3072
	v_mul_f32_e32 v116, v24, v116
	v_mul_f32_e32 v117, v24, v117
	v_mul_f32_e32 v118, v24, v118
	v_mul_f32_e32 v119, v24, v119
	ds_write_b128 v4, v[116:119] offset:4096
	v_mul_f32_e32 v120, v25, v120
	v_mul_f32_e32 v121, v25, v121
	v_mul_f32_e32 v122, v25, v122
	v_mul_f32_e32 v123, v25, v123
	ds_write_b128 v4, v[120:123] offset:5120
	v_mul_f32_e32 v124, v26, v124
	v_mul_f32_e32 v125, v26, v125
	v_mul_f32_e32 v126, v26, v126
	v_mul_f32_e32 v127, v26, v127
	ds_write_b128 v4, v[124:127] offset:6144
	v_mul_f32_e32 v128, v27, v128
	v_mul_f32_e32 v129, v27, v129
	v_mul_f32_e32 v130, v27, v130
	v_mul_f32_e32 v131, v27, v131
	ds_write_b128 v4, v[128:131] offset:7168
	s_waitcnt lgkmcnt(0)
	s_barrier
; #define GAS __attribute__((address_space(1)))
; #define LAS __attribute__((address_space(3)))
; #define LDS_WAIT() asm volatile("s_waitcnt lgkmcnt(0)" ::: "memory")
;     const int pr = item >> 1, kb = 2 * (pr / nblk) + (item & 1), nb = pr % nblk, k0 = 64 * kb, n0 = 32 * nb;
;     const int nr = n0 + (lane & 31); const int sc = MAP == 1 ? src_col_in(nr) : nr;
;     float v[32];
; #pragma unroll
;     for (int i = 0; i < 32; ++i) v[i] = sc >= 0 ? W[(size_t)(k0 + 2 * i + (lane >> 5)) * Nsrc + sc] : 0.f;
; #pragma unroll
;     for (int i = 0; i < 32; ++i) { const int k = k0 + 2 * i + (lane >> 5); float x = v[i] * wscale; if (KS) x *= (k < ksplit ? ksA[k] : ksB[k - ksplit]); scr[(2 * i + (lane >> 5)) * 33 + (lane & 31)] = x; }
;     LDS_WAIT(); asm volatile("" ::: "memory");
;     const int c = lane & 7;
; #pragma unroll
;     for (int j = 0; j < 4; ++j) { const int n = (lane >> 3) + 8 * j; const LAS float* s = scr + (8 * c) * 33 + n;
;         const unsigned long long o = (unsigned long long)pg8::pk4_fp8(s[0 * 33], s[1 * 33], s[2 * 33], s[3 * 33]) | ((unsigned long long)pg8::pk4_fp8(s[4 * 33], s[5 * 33], s[6 * 33], s[7 * 33]) << 32);
;         *(GAS unsigned long long*)(WT + (size_t)(n0 + n) * K + k0 + 8 * c) = o; }
;     LDS_WAIT(); asm volatile("" ::: "memory");
; __global__ void __launch_bounds__(NWAVES * 64, 2) hybrid_fwd(Args args) {
;     ...
;             if (r < I_O) { if (l >= WO_F8_FROM) p0_transpose_item_f8<true>(args.in[13] + (size_t)l * DM * DM, DM, DM, DM / 32, (unsigned char*)(ws + WS_WO + l * SZ_WO), 64.f, args.in[6] + l * 2048, args.in[12] + l * 2048, 2048, scr, r, lane);
;                 else p0_transpose_item<0, true>(args.in[13] + (size_t)l * DM * DM, DM, DM, DM / 32, (bf16*)(ws + WS_WO + l * SZ_WO), args.in[6] + l * 2048, args.in[12] + l * 2048, 2048, scr, r, lane); continue; } r -= I_O;
;             if (r < I_UP) { p0_transpose_item_f8<true>(args.in[15] + (size_t)l * DM * FF, DM, FF, FF / 32, (unsigned char*)(ws + WS_WUP + l * SZ_WUP), WUP8_SCALE, args.in[14] + l * DM, args.in[14] + l * DM, DM, scr, r, lane); continue; } r -= I_UP;
;             p0_transpose_item_f8<false>(args.in[16] + (size_t)l * FF * DM, FF, DM, DM / 32, (unsigned char*)(ws + WS_WDN + l * SZ_WDN), 128.f, args.in[16], args.in[16], 0, scr, r, lane);
	s_add_i32 s19, s39, 21
	s_min_u32 s19, s19, 31
	s_lshl_b32 s19, s19, 19
	s_add_u32 s14, s50, s19
	s_addc_u32 s15, s51, 0
	ds_read_b32 v170, v6
	ds_read_b32 v171, v6 offset:512
	ds_read_b32 v172, v6 offset:1024
	ds_read_b32 v173, v6 offset:1536
	ds_read_b32 v174, v6 offset:2048
	ds_read_b32 v175, v6 offset:2560
	ds_read_b32 v176, v6 offset:3072
	ds_read_b32 v177, v6 offset:3584
	ds_read_b32 v196, v6 offset:4096
	ds_read_b32 v197, v6 offset:4608
	ds_read_b32 v198, v6 offset:5120
	ds_read_b32 v199, v6 offset:5632
	ds_read_b32 v200, v6 offset:6144
	ds_read_b32 v201, v6 offset:6656
	ds_read_b32 v202, v6 offset:7168
	ds_read_b32 v203, v6 offset:7680
	s_waitcnt lgkmcnt(0)
	v_max_f32_e32 v170, v170, v170
	v_max_f32_e32 v171, v171, v171
	v_max_f32_e32 v172, v172, v172
	v_max_f32_e32 v173, v173, v173
	v_max_f32_e32 v174, v174, v174
	v_max_f32_e32 v175, v175, v175
	v_max_f32_e32 v176, v176, v176
	v_max_f32_e32 v177, v177, v177
	v_max_f32_e32 v196, v196, v196
	v_max_f32_e32 v197, v197, v197
	v_max_f32_e32 v198, v198, v198
	v_max_f32_e32 v199, v199, v199
	v_max_f32_e32 v200, v200, v200
	v_max_f32_e32 v201, v201, v201
	v_max_f32_e32 v202, v202, v202
	v_max_f32_e32 v203, v203, v203
	v_med3_f32 v170, v170, s20, v13
	v_med3_f32 v171, v171, s20, v13
	v_med3_f32 v172, v172, s20, v13
	v_med3_f32 v173, v173, s20, v13
	v_med3_f32 v174, v174, s20, v13
	v_med3_f32 v175, v175, s20, v13
	v_med3_f32 v176, v176, s20, v13
	v_med3_f32 v177, v177, s20, v13
	v_med3_f32 v196, v196, s20, v13
	v_med3_f32 v197, v197, s20, v13
	v_med3_f32 v198, v198, s20, v13
	v_med3_f32 v199, v199, s20, v13
	v_med3_f32 v200, v200, s20, v13
	v_med3_f32 v201, v201, s20, v13
	v_med3_f32 v202, v202, s20, v13
	v_med3_f32 v203, v203, s20, v13
	v_mov_b32_e32 v208, 0
	v_mov_b32_e32 v209, 0
	v_mov_b32_e32 v210, 0
	v_mov_b32_e32 v211, 0
	v_cvt_pk_fp8_f32 v208, v170, v171
	v_cvt_pk_fp8_f32 v209, v174, v175
	v_cvt_pk_fp8_f32 v210, v196, v197
	v_cvt_pk_fp8_f32 v211, v200, v201
	v_cvt_pk_fp8_f32 v208, v172, v173 op_sel:[0,0,1]
	v_cvt_pk_fp8_f32 v209, v176, v177 op_sel:[0,0,1]
	v_cvt_pk_fp8_f32 v210, v198, v199 op_sel:[0,0,1]
	v_cvt_pk_fp8_f32 v211, v202, v203 op_sel:[0,0,1]
	s_nop 0
	global_store_dwordx4 v28, v[208:211], s[14:15]
	ds_read_b32 v170, v8
	ds_read_b32 v171, v8 offset:512
	ds_read_b32 v172, v8 offset:1024
	ds_read_b32 v173, v8 offset:1536
	ds_read_b32 v174, v8 offset:2048
	ds_read_b32 v175, v8 offset:2560
	ds_read_b32 v176, v8 offset:3072
	ds_read_b32 v177, v8 offset:3584
	ds_read_b32 v196, v8 offset:4096
	ds_read_b32 v197, v8 offset:4608
	ds_read_b32 v198, v8 offset:5120
	ds_read_b32 v199, v8 offset:5632
	ds_read_b32 v200, v8 offset:6144
	ds_read_b32 v201, v8 offset:6656
	ds_read_b32 v202, v8 offset:7168
	ds_read_b32 v203, v8 offset:7680
	s_waitcnt lgkmcnt(0)
	v_max_f32_e32 v170, v170, v170
	v_max_f32_e32 v171, v171, v171
	v_max_f32_e32 v172, v172, v172
	v_max_f32_e32 v173, v173, v173
	v_max_f32_e32 v174, v174, v174
	v_max_f32_e32 v175, v175, v175
	v_max_f32_e32 v176, v176, v176
	v_max_f32_e32 v177, v177, v177
	v_max_f32_e32 v196, v196, v196
	v_max_f32_e32 v197, v197, v197
	v_max_f32_e32 v198, v198, v198
	v_max_f32_e32 v199, v199, v199
	v_max_f32_e32 v200, v200, v200
	v_max_f32_e32 v201, v201, v201
	v_max_f32_e32 v202, v202, v202
	v_max_f32_e32 v203, v203, v203
	v_med3_f32 v170, v170, s20, v13
	v_med3_f32 v171, v171, s20, v13
	v_med3_f32 v172, v172, s20, v13
	v_med3_f32 v173, v173, s20, v13
	v_med3_f32 v174, v174, s20, v13
	v_med3_f32 v175, v175, s20, v13
	v_med3_f32 v176, v176, s20, v13
	v_med3_f32 v177, v177, s20, v13
	v_med3_f32 v196, v196, s20, v13
	v_med3_f32 v197, v197, s20, v13
	v_med3_f32 v198, v198, s20, v13
	v_med3_f32 v199, v199, s20, v13
	v_med3_f32 v200, v200, s20, v13
	v_med3_f32 v201, v201, s20, v13
	v_med3_f32 v202, v202, s20, v13
	v_med3_f32 v203, v203, s20, v13
	v_mov_b32_e32 v208, 0
	v_mov_b32_e32 v209, 0
	v_mov_b32_e32 v210, 0
	v_mov_b32_e32 v211, 0
	v_cvt_pk_fp8_f32 v208, v170, v171
	v_cvt_pk_fp8_f32 v209, v174, v175
	v_cvt_pk_fp8_f32 v210, v196, v197
	v_cvt_pk_fp8_f32 v211, v200, v201
	v_cvt_pk_fp8_f32 v208, v172, v173 op_sel:[0,0,1]
	v_cvt_pk_fp8_f32 v209, v176, v177 op_sel:[0,0,1]
	v_cvt_pk_fp8_f32 v210, v198, v199 op_sel:[0,0,1]
	v_cvt_pk_fp8_f32 v211, v202, v203 op_sel:[0,0,1]
	s_nop 0
	global_store_dwordx4 v29, v[208:211], s[14:15]
	s_waitcnt vmcnt(24)
	v_mul_f32_e32 v132, v20, v132
	v_mul_f32_e32 v133, v20, v133
	v_mul_f32_e32 v134, v20, v134
	v_mul_f32_e32 v135, v20, v135
	ds_write_b128 v5, v[132:135]
	v_mul_f32_e32 v136, v21, v136
	v_mul_f32_e32 v137, v21, v137
	v_mul_f32_e32 v138, v21, v138
	v_mul_f32_e32 v139, v21, v139
	ds_write_b128 v5, v[136:139] offset:1024
	v_mul_f32_e32 v140, v22, v140
	v_mul_f32_e32 v141, v22, v141
	v_mul_f32_e32 v142, v22, v142
	v_mul_f32_e32 v143, v22, v143
	ds_write_b128 v5, v[140:143] offset:2048
	v_mul_f32_e32 v144, v23, v144
	v_mul_f32_e32 v145, v23, v145
	v_mul_f32_e32 v146, v23, v146
	v_mul_f32_e32 v147, v23, v147
	ds_write_b128 v5, v[144:147] offset:3072
	v_mul_f32_e32 v148, v24, v148
	v_mul_f32_e32 v149, v24, v149
	v_mul_f32_e32 v150, v24, v150
	v_mul_f32_e32 v151, v24, v151
	ds_write_b128 v5, v[148:151] offset:4096
	v_mul_f32_e32 v152, v25, v152
	v_mul_f32_e32 v153, v25, v153
	v_mul_f32_e32 v154, v25, v154
	v_mul_f32_e32 v155, v25, v155
	ds_write_b128 v5, v[152:155] offset:5120
	v_mul_f32_e32 v156, v26, v156
	v_mul_f32_e32 v157, v26, v157
	v_mul_f32_e32 v158, v26, v158
	v_mul_f32_e32 v159, v26, v159
	ds_write_b128 v5, v[156:159] offset:6144
	v_mul_f32_e32 v160, v27, v160
	v_mul_f32_e32 v161, v27, v161
	v_mul_f32_e32 v162, v27, v162
	v_mul_f32_e32 v163, v27, v163
	ds_write_b128 v5, v[160:163] offset:7168
	s_waitcnt lgkmcnt(0)
	s_barrier
; #define GAS __attribute__((address_space(1)))
; #define LAS __attribute__((address_space(3)))
; #define LDS_WAIT() asm volatile("s_waitcnt lgkmcnt(0)" ::: "memory")
;     const int pr = item >> 1, kb = 2 * (pr / nblk) + (item & 1), nb = pr % nblk, k0 = 64 * kb, n0 = 32 * nb;
;     const int nr = n0 + (lane & 31); const int sc = MAP == 1 ? src_col_in(nr) : nr;
;     float v[32];
; #pragma unroll
;     for (int i = 0; i < 32; ++i) v[i] = sc >= 0 ? W[(size_t)(k0 + 2 * i + (lane >> 5)) * Nsrc + sc] : 0.f;
; #pragma unroll
;     for (int i = 0; i < 32; ++i) { const int k = k0 + 2 * i + (lane >> 5); float x = v[i] * wscale; if (KS) x *= (k < ksplit ? ksA[k] : ksB[k - ksplit]); scr[(2 * i + (lane >> 5)) * 33 + (lane & 31)] = x; }
;     LDS_WAIT(); asm volatile("" ::: "memory");
;     const int c = lane & 7;
; #pragma unroll
;     for (int j = 0; j < 4; ++j) { const int n = (lane >> 3) + 8 * j; const LAS float* s = scr + (8 * c) * 33 + n;
;         const unsigned long long o = (unsigned long long)pg8::pk4_fp8(s[0 * 33], s[1 * 33], s[2 * 33], s[3 * 33]) | ((unsigned long long)pg8::pk4_fp8(s[4 * 33], s[5 * 33], s[6 * 33], s[7 * 33]) << 32);
;         *(GAS unsigned long long*)(WT + (size_t)(n0 + n) * K + k0 + 8 * c) = o; }
;     LDS_WAIT(); asm volatile("" ::: "memory");
; __global__ void __launch_bounds__(NWAVES * 64, 2) hybrid_fwd(Args args) {
;     ...
;             if (r < I_O) { if (l >= WO_F8_FROM) p0_transpose_item_f8<true>(args.in[13] + (size_t)l * DM * DM, DM, DM, DM / 32, (unsigned char*)(ws + WS_WO + l * SZ_WO), 64.f, args.in[6] + l * 2048, args.in[12] + l * 2048, 2048, scr, r, lane);
;                 else p0_transpose_item<0, true>(args.in[13] + (size_t)l * DM * DM, DM, DM, DM / 32, (bf16*)(ws + WS_WO + l * SZ_WO), args.in[6] + l * 2048, args.in[12] + l * 2048, 2048, scr, r, lane); continue; } r -= I_O;
;             if (r < I_UP) { p0_transpose_item_f8<true>(args.in[15] + (size_t)l * DM * FF, DM, FF, FF / 32, (unsigned char*)(ws + WS_WUP + l * SZ_WUP), WUP8_SCALE, args.in[14] + l * DM, args.in[14] + l * DM, DM, scr, r, lane); continue; } r -= I_UP;
;             p0_transpose_item_f8<false>(args.in[16] + (size_t)l * FF * DM, FF, DM, DM / 32, (unsigned char*)(ws + WS_WDN + l * SZ_WDN), 128.f, args.in[16], args.in[16], 0, scr, r, lane);
	s_add_i32 s19, s39, 24
	s_min_u32 s19, s19, 31
	s_lshl_b32 s19, s19, 19
	s_add_u32 s14, s50, s19
	s_addc_u32 s15, s51, 0
	ds_read_b32 v170, v7
	ds_read_b32 v171, v7 offset:512
	ds_read_b32 v172, v7 offset:1024
	ds_read_b32 v173, v7 offset:1536
	ds_read_b32 v174, v7 offset:2048
	ds_read_b32 v175, v7 offset:2560
	ds_read_b32 v176, v7 offset:3072
	ds_read_b32 v177, v7 offset:3584
	ds_read_b32 v196, v7 offset:4096
	ds_read_b32 v197, v7 offset:4608
	ds_read_b32 v198, v7 offset:5120
	ds_read_b32 v199, v7 offset:5632
	ds_read_b32 v200, v7 offset:6144
	ds_read_b32 v201, v7 offset:6656
	ds_read_b32 v202, v7 offset:7168
	ds_read_b32 v203, v7 offset:7680
	s_waitcnt lgkmcnt(0)
	v_max_f32_e32 v170, v170, v170
	v_max_f32_e32 v171, v171, v171
	v_max_f32_e32 v172, v172, v172
	v_max_f32_e32 v173, v173, v173
	v_max_f32_e32 v174, v174, v174
	v_max_f32_e32 v175, v175, v175
	v_max_f32_e32 v176, v176, v176
	v_max_f32_e32 v177, v177, v177
	v_max_f32_e32 v196, v196, v196
	v_max_f32_e32 v197, v197, v197
	v_max_f32_e32 v198, v198, v198
	v_max_f32_e32 v199, v199, v199
	v_max_f32_e32 v200, v200, v200
	v_max_f32_e32 v201, v201, v201
	v_max_f32_e32 v202, v202, v202
	v_max_f32_e32 v203, v203, v203
	v_med3_f32 v170, v170, s20, v13
	v_med3_f32 v171, v171, s20, v13
	v_med3_f32 v172, v172, s20, v13
	v_med3_f32 v173, v173, s20, v13
	v_med3_f32 v174, v174, s20, v13
	v_med3_f32 v175, v175, s20, v13
	v_med3_f32 v176, v176, s20, v13
	v_med3_f32 v177, v177, s20, v13
	v_med3_f32 v196, v196, s20, v13
	v_med3_f32 v197, v197, s20, v13
	v_med3_f32 v198, v198, s20, v13
	v_med3_f32 v199, v199, s20, v13
	v_med3_f32 v200, v200, s20, v13
	v_med3_f32 v201, v201, s20, v13
	v_med3_f32 v202, v202, s20, v13
	v_med3_f32 v203, v203, s20, v13
	v_mov_b32_e32 v208, 0
	v_mov_b32_e32 v209, 0
	v_mov_b32_e32 v210, 0
	v_mov_b32_e32 v211, 0
	v_cvt_pk_fp8_f32 v208, v170, v171
	v_cvt_pk_fp8_f32 v209, v174, v175
	v_cvt_pk_fp8_f32 v210, v196, v197
	v_cvt_pk_fp8_f32 v211, v200, v201
	v_cvt_pk_fp8_f32 v208, v172, v173 op_sel:[0,0,1]
	v_cvt_pk_fp8_f32 v209, v176, v177 op_sel:[0,0,1]
	v_cvt_pk_fp8_f32 v210, v198, v199 op_sel:[0,0,1]
	v_cvt_pk_fp8_f32 v211, v202, v203 op_sel:[0,0,1]
	s_nop 0
	global_store_dwordx4 v28, v[208:211], s[14:15]
	ds_read_b32 v170, v9
	ds_read_b32 v171, v9 offset:512
	ds_read_b32 v172, v9 offset:1024
	ds_read_b32 v173, v9 offset:1536
	ds_read_b32 v174, v9 offset:2048
	ds_read_b32 v175, v9 offset:2560
	ds_read_b32 v176, v9 offset:3072
	ds_read_b32 v177, v9 offset:3584
	ds_read_b32 v196, v9 offset:4096
	ds_read_b32 v197, v9 offset:4608
	ds_read_b32 v198, v9 offset:5120
	ds_read_b32 v199, v9 offset:5632
	ds_read_b32 v200, v9 offset:6144
	ds_read_b32 v201, v9 offset:6656
	ds_read_b32 v202, v9 offset:7168
	ds_read_b32 v203, v9 offset:7680
	s_waitcnt lgkmcnt(0)
	v_max_f32_e32 v170, v170, v170
	v_max_f32_e32 v171, v171, v171
	v_max_f32_e32 v172, v172, v172
	v_max_f32_e32 v173, v173, v173
	v_max_f32_e32 v174, v174, v174
	v_max_f32_e32 v175, v175, v175
	v_max_f32_e32 v176, v176, v176
	v_max_f32_e32 v177, v177, v177
	v_max_f32_e32 v196, v196, v196
	v_max_f32_e32 v197, v197, v197
	v_max_f32_e32 v198, v198, v198
	v_max_f32_e32 v199, v199, v199
	v_max_f32_e32 v200, v200, v200
	v_max_f32_e32 v201, v201, v201
	v_max_f32_e32 v202, v202, v202
	v_max_f32_e32 v203, v203, v203
	v_med3_f32 v170, v170, s20, v13
	v_med3_f32 v171, v171, s20, v13
	v_med3_f32 v172, v172, s20, v13
	v_med3_f32 v173, v173, s20, v13
	v_med3_f32 v174, v174, s20, v13
	v_med3_f32 v175, v175, s20, v13
	v_med3_f32 v176, v176, s20, v13
	v_med3_f32 v177, v177, s20, v13
	v_med3_f32 v196, v196, s20, v13
	v_med3_f32 v197, v197, s20, v13
	v_med3_f32 v198, v198, s20, v13
	v_med3_f32 v199, v199, s20, v13
	v_med3_f32 v200, v200, s20, v13
	v_med3_f32 v201, v201, s20, v13
	v_med3_f32 v202, v202, s20, v13
	v_med3_f32 v203, v203, s20, v13
	v_mov_b32_e32 v208, 0
	v_mov_b32_e32 v209, 0
	v_mov_b32_e32 v210, 0
	v_mov_b32_e32 v211, 0
	v_cvt_pk_fp8_f32 v208, v170, v171
	v_cvt_pk_fp8_f32 v209, v174, v175
	v_cvt_pk_fp8_f32 v210, v196, v197
	v_cvt_pk_fp8_f32 v211, v200, v201
	v_cvt_pk_fp8_f32 v208, v172, v173 op_sel:[0,0,1]
	v_cvt_pk_fp8_f32 v209, v176, v177 op_sel:[0,0,1]
	v_cvt_pk_fp8_f32 v210, v198, v199 op_sel:[0,0,1]
	v_cvt_pk_fp8_f32 v211, v202, v203 op_sel:[0,0,1]
	s_nop 0
	global_store_dwordx4 v29, v[208:211], s[14:15]
	s_waitcnt vmcnt(16)
	v_mul_f32_e32 v36, v20, v36
	v_mul_f32_e32 v37, v20, v37
	v_mul_f32_e32 v38, v20, v38
	v_mul_f32_e32 v39, v20, v39
	ds_write_b128 v4, v[36:39]
	v_mul_f32_e32 v40, v21, v40
	v_mul_f32_e32 v41, v21, v41
	v_mul_f32_e32 v42, v21, v42
	v_mul_f32_e32 v43, v21, v43
	ds_write_b128 v4, v[40:43] offset:1024
	v_mul_f32_e32 v44, v22, v44
	v_mul_f32_e32 v45, v22, v45
	v_mul_f32_e32 v46, v22, v46
	v_mul_f32_e32 v47, v22, v47
	ds_write_b128 v4, v[44:47] offset:2048
	v_mul_f32_e32 v48, v23, v48
	v_mul_f32_e32 v49, v23, v49
	v_mul_f32_e32 v50, v23, v50
	v_mul_f32_e32 v51, v23, v51
	ds_write_b128 v4, v[48:51] offset:3072
	v_mul_f32_e32 v52, v24, v52
	v_mul_f32_e32 v53, v24, v53
	v_mul_f32_e32 v54, v24, v54
	v_mul_f32_e32 v55, v24, v55
	ds_write_b128 v4, v[52:55] offset:4096
	v_mul_f32_e32 v56, v25, v56
	v_mul_f32_e32 v57, v25, v57
	v_mul_f32_e32 v58, v25, v58
	v_mul_f32_e32 v59, v25, v59
	ds_write_b128 v4, v[56:59] offset:5120
	v_mul_f32_e32 v60, v26, v60
	v_mul_f32_e32 v61, v26, v61
	v_mul_f32_e32 v62, v26, v62
	v_mul_f32_e32 v63, v26, v63
	ds_write_b128 v4, v[60:63] offset:6144
	v_mul_f32_e32 v64, v27, v64
	v_mul_f32_e32 v65, v27, v65
	v_mul_f32_e32 v66, v27, v66
	v_mul_f32_e32 v67, v27, v67
	ds_write_b128 v4, v[64:67] offset:7168
	s_waitcnt lgkmcnt(0)
	s_barrier
; #define GAS __attribute__((address_space(1)))
; #define LAS __attribute__((address_space(3)))
; #define LDS_WAIT() asm volatile("s_waitcnt lgkmcnt(0)" ::: "memory")
;     const int pr = item >> 1, kb = 2 * (pr / nblk) + (item & 1), nb = pr % nblk, k0 = 64 * kb, n0 = 32 * nb;
;     const int nr = n0 + (lane & 31); const int sc = MAP == 1 ? src_col_in(nr) : nr;
;     float v[32];
; #pragma unroll
;     for (int i = 0; i < 32; ++i) v[i] = sc >= 0 ? W[(size_t)(k0 + 2 * i + (lane >> 5)) * Nsrc + sc] : 0.f;
; #pragma unroll
;     for (int i = 0; i < 32; ++i) { const int k = k0 + 2 * i + (lane >> 5); float x = v[i] * wscale; if (KS) x *= (k < ksplit ? ksA[k] : ksB[k - ksplit]); scr[(2 * i + (lane >> 5)) * 33 + (lane & 31)] = x; }
;     LDS_WAIT(); asm volatile("" ::: "memory");
;     const int c = lane & 7;
; #pragma unroll
;     for (int j = 0; j < 4; ++j) { const int n = (lane >> 3) + 8 * j; const LAS float* s = scr + (8 * c) * 33 + n;
;         const unsigned long long o = (unsigned long long)pg8::pk4_fp8(s[0 * 33], s[1 * 33], s[2 * 33], s[3 * 33]) | ((unsigned long long)pg8::pk4_fp8(s[4 * 33], s[5 * 33], s[6 * 33], s[7 * 33]) << 32);
;         *(GAS unsigned long long*)(WT + (size_t)(n0 + n) * K + k0 + 8 * c) = o; }
;     LDS_WAIT(); asm volatile("" ::: "memory");
; __global__ void __launch_bounds__(NWAVES * 64, 2) hybrid_fwd(Args args) {
;     ...
;             if (r < I_O) { if (l >= WO_F8_FROM) p0_transpose_item_f8<true>(args.in[13] + (size_t)l * DM * DM, DM, DM, DM / 32, (unsigned char*)(ws + WS_WO + l * SZ_WO), 64.f, args.in[6] + l * 2048, args.in[12] + l * 2048, 2048, scr, r, lane);
;                 else p0_transpose_item<0, true>(args.in[13] + (size_t)l * DM * DM, DM, DM, DM / 32, (bf16*)(ws + WS_WO + l * SZ_WO), args.in[6] + l * 2048, args.in[12] + l * 2048, 2048, scr, r, lane); continue; } r -= I_O;
;             if (r < I_UP) { p0_transpose_item_f8<true>(args.in[15] + (size_t)l * DM * FF, DM, FF, FF / 32, (unsigned char*)(ws + WS_WUP + l * SZ_WUP), WUP8_SCALE, args.in[14] + l * DM, args.in[14] + l * DM, DM, scr, r, lane); continue; } r -= I_UP;
;             p0_transpose_item_f8<false>(args.in[16] + (size_t)l * FF * DM, FF, DM, DM / 32, (unsigned char*)(ws + WS_WDN + l * SZ_WDN), 128.f, args.in[16], args.in[16], 0, scr, r, lane);
	s_add_i32 s19, s39, 27
	s_min_u32 s19, s19, 31
	s_lshl_b32 s19, s19, 19
	s_add_u32 s14, s50, s19
	s_addc_u32 s15, s51, 0
	ds_read_b32 v170, v6
	ds_read_b32 v171, v6 offset:512
	ds_read_b32 v172, v6 offset:1024
	ds_read_b32 v173, v6 offset:1536
	ds_read_b32 v174, v6 offset:2048
	ds_read_b32 v175, v6 offset:2560
	ds_read_b32 v176, v6 offset:3072
	ds_read_b32 v177, v6 offset:3584
	ds_read_b32 v196, v6 offset:4096
	ds_read_b32 v197, v6 offset:4608
	ds_read_b32 v198, v6 offset:5120
	ds_read_b32 v199, v6 offset:5632
	ds_read_b32 v200, v6 offset:6144
	ds_read_b32 v201, v6 offset:6656
	ds_read_b32 v202, v6 offset:7168
	ds_read_b32 v203, v6 offset:7680
	s_waitcnt lgkmcnt(0)
	v_max_f32_e32 v170, v170, v170
	v_max_f32_e32 v171, v171, v171
	v_max_f32_e32 v172, v172, v172
	v_max_f32_e32 v173, v173, v173
	v_max_f32_e32 v174, v174, v174
	v_max_f32_e32 v175, v175, v175
	v_max_f32_e32 v176, v176, v176
	v_max_f32_e32 v177, v177, v177
	v_max_f32_e32 v196, v196, v196
	v_max_f32_e32 v197, v197, v197
	v_max_f32_e32 v198, v198, v198
	v_max_f32_e32 v199, v199, v199
	v_max_f32_e32 v200, v200, v200
	v_max_f32_e32 v201, v201, v201
	v_max_f32_e32 v202, v202, v202
	v_max_f32_e32 v203, v203, v203
	v_med3_f32 v170, v170, s20, v13
	v_med3_f32 v171, v171, s20, v13
	v_med3_f32 v172, v172, s20, v13
	v_med3_f32 v173, v173, s20, v13
	v_med3_f32 v174, v174, s20, v13
	v_med3_f32 v175, v175, s20, v13
	v_med3_f32 v176, v176, s20, v13
	v_med3_f32 v177, v177, s20, v13
	v_med3_f32 v196, v196, s20, v13
	v_med3_f32 v197, v197, s20, v13
	v_med3_f32 v198, v198, s20, v13
	v_med3_f32 v199, v199, s20, v13
	v_med3_f32 v200, v200, s20, v13
	v_med3_f32 v201, v201, s20, v13
	v_med3_f32 v202, v202, s20, v13
	v_med3_f32 v203, v203, s20, v13
	v_mov_b32_e32 v208, 0
	v_mov_b32_e32 v209, 0
	v_mov_b32_e32 v210, 0
	v_mov_b32_e32 v211, 0
	v_cvt_pk_fp8_f32 v208, v170, v171
	v_cvt_pk_fp8_f32 v209, v174, v175
	v_cvt_pk_fp8_f32 v210, v196, v197
	v_cvt_pk_fp8_f32 v211, v200, v201
	v_cvt_pk_fp8_f32 v208, v172, v173 op_sel:[0,0,1]
	v_cvt_pk_fp8_f32 v209, v176, v177 op_sel:[0,0,1]
	v_cvt_pk_fp8_f32 v210, v198, v199 op_sel:[0,0,1]
	v_cvt_pk_fp8_f32 v211, v202, v203 op_sel:[0,0,1]
	s_nop 0
	global_store_dwordx4 v28, v[208:211], s[14:15]
	ds_read_b32 v170, v8
	ds_read_b32 v171, v8 offset:512
	ds_read_b32 v172, v8 offset:1024
	ds_read_b32 v173, v8 offset:1536
	ds_read_b32 v174, v8 offset:2048
	ds_read_b32 v175, v8 offset:2560
	ds_read_b32 v176, v8 offset:3072
	ds_read_b32 v177, v8 offset:3584
	ds_read_b32 v196, v8 offset:4096
	ds_read_b32 v197, v8 offset:4608
	ds_read_b32 v198, v8 offset:5120
	ds_read_b32 v199, v8 offset:5632
	ds_read_b32 v200, v8 offset:6144
	ds_read_b32 v201, v8 offset:6656
	ds_read_b32 v202, v8 offset:7168
	ds_read_b32 v203, v8 offset:7680
	s_waitcnt lgkmcnt(0)
	v_max_f32_e32 v170, v170, v170
	v_max_f32_e32 v171, v171, v171
	v_max_f32_e32 v172, v172, v172
	v_max_f32_e32 v173, v173, v173
	v_max_f32_e32 v174, v174, v174
	v_max_f32_e32 v175, v175, v175
	v_max_f32_e32 v176, v176, v176
	v_max_f32_e32 v177, v177, v177
	v_max_f32_e32 v196, v196, v196
	v_max_f32_e32 v197, v197, v197
	v_max_f32_e32 v198, v198, v198
	v_max_f32_e32 v199, v199, v199
	v_max_f32_e32 v200, v200, v200
	v_max_f32_e32 v201, v201, v201
	v_max_f32_e32 v202, v202, v202
	v_max_f32_e32 v203, v203, v203
	v_med3_f32 v170, v170, s20, v13
	v_med3_f32 v171, v171, s20, v13
	v_med3_f32 v172, v172, s20, v13
	v_med3_f32 v173, v173, s20, v13
	v_med3_f32 v174, v174, s20, v13
	v_med3_f32 v175, v175, s20, v13
	v_med3_f32 v176, v176, s20, v13
	v_med3_f32 v177, v177, s20, v13
	v_med3_f32 v196, v196, s20, v13
	v_med3_f32 v197, v197, s20, v13
	v_med3_f32 v198, v198, s20, v13
	v_med3_f32 v199, v199, s20, v13
	v_med3_f32 v200, v200, s20, v13
	v_med3_f32 v201, v201, s20, v13
	v_med3_f32 v202, v202, s20, v13
	v_med3_f32 v203, v203, s20, v13
	v_mov_b32_e32 v208, 0
	v_mov_b32_e32 v209, 0
	v_mov_b32_e32 v210, 0
	v_mov_b32_e32 v211, 0
	v_cvt_pk_fp8_f32 v208, v170, v171
	v_cvt_pk_fp8_f32 v209, v174, v175
	v_cvt_pk_fp8_f32 v210, v196, v197
	v_cvt_pk_fp8_f32 v211, v200, v201
	v_cvt_pk_fp8_f32 v208, v172, v173 op_sel:[0,0,1]
	v_cvt_pk_fp8_f32 v209, v176, v177 op_sel:[0,0,1]
	v_cvt_pk_fp8_f32 v210, v198, v199 op_sel:[0,0,1]
	v_cvt_pk_fp8_f32 v211, v202, v203 op_sel:[0,0,1]
	s_nop 0
	global_store_dwordx4 v29, v[208:211], s[14:15]
	s_waitcnt vmcnt(8)
	v_mul_f32_e32 v68, v20, v68
	v_mul_f32_e32 v69, v20, v69
	v_mul_f32_e32 v70, v20, v70
	v_mul_f32_e32 v71, v20, v71
	ds_write_b128 v5, v[68:71]
	v_mul_f32_e32 v72, v21, v72
	v_mul_f32_e32 v73, v21, v73
	v_mul_f32_e32 v74, v21, v74
	v_mul_f32_e32 v75, v21, v75
	ds_write_b128 v5, v[72:75] offset:1024
	v_mul_f32_e32 v76, v22, v76
	v_mul_f32_e32 v77, v22, v77
	v_mul_f32_e32 v78, v22, v78
	v_mul_f32_e32 v79, v22, v79
	ds_write_b128 v5, v[76:79] offset:2048
	v_mul_f32_e32 v80, v23, v80
	v_mul_f32_e32 v81, v23, v81
	v_mul_f32_e32 v82, v23, v82
	v_mul_f32_e32 v83, v23, v83
	ds_write_b128 v5, v[80:83] offset:3072
	v_mul_f32_e32 v84, v24, v84
	v_mul_f32_e32 v85, v24, v85
	v_mul_f32_e32 v86, v24, v86
	v_mul_f32_e32 v87, v24, v87
	ds_write_b128 v5, v[84:87] offset:4096
	v_mul_f32_e32 v88, v25, v88
	v_mul_f32_e32 v89, v25, v89
	v_mul_f32_e32 v90, v25, v90
	v_mul_f32_e32 v91, v25, v91
	ds_write_b128 v5, v[88:91] offset:5120
	v_mul_f32_e32 v92, v26, v92
	v_mul_f32_e32 v93, v26, v93
	v_mul_f32_e32 v94, v26, v94
	v_mul_f32_e32 v95, v26, v95
	ds_write_b128 v5, v[92:95] offset:6144
	v_mul_f32_e32 v96, v27, v96
	v_mul_f32_e32 v97, v27, v97
	v_mul_f32_e32 v98, v27, v98
	v_mul_f32_e32 v99, v27, v99
	ds_write_b128 v5, v[96:99] offset:7168
	s_waitcnt lgkmcnt(0)
	s_barrier
; #define GAS __attribute__((address_space(1)))
; #define LAS __attribute__((address_space(3)))
; #define LDS_WAIT() asm volatile("s_waitcnt lgkmcnt(0)" ::: "memory")
;     const int pr = item >> 1, kb = 2 * (pr / nblk) + (item & 1), nb = pr % nblk, k0 = 64 * kb, n0 = 32 * nb;
;     const int nr = n0 + (lane & 31); const int sc = MAP == 1 ? src_col_in(nr) : nr;
;     float v[32];
; #pragma unroll
;     for (int i = 0; i < 32; ++i) v[i] = sc >= 0 ? W[(size_t)(k0 + 2 * i + (lane >> 5)) * Nsrc + sc] : 0.f;
; #pragma unroll
;     for (int i = 0; i < 32; ++i) { const int k = k0 + 2 * i + (lane >> 5); float x = v[i] * wscale; if (KS) x *= (k < ksplit ? ksA[k] : ksB[k - ksplit]); scr[(2 * i + (lane >> 5)) * 33 + (lane & 31)] = x; }
;     LDS_WAIT(); asm volatile("" ::: "memory");
;     const int c = lane & 7;
; #pragma unroll
;     for (int j = 0; j < 4; ++j) { const int n = (lane >> 3) + 8 * j; const LAS float* s = scr + (8 * c) * 33 + n;
;         const unsigned long long o = (unsigned long long)pg8::pk4_fp8(s[0 * 33], s[1 * 33], s[2 * 33], s[3 * 33]) | ((unsigned long long)pg8::pk4_fp8(s[4 * 33], s[5 * 33], s[6 * 33], s[7 * 33]) << 32);
;         *(GAS unsigned long long*)(WT + (size_t)(n0 + n) * K + k0 + 8 * c) = o; }
;     LDS_WAIT(); asm volatile("" ::: "memory");
; __global__ void __launch_bounds__(NWAVES * 64, 2) hybrid_fwd(Args args) {
;     ...
;             if (r < I_O) { if (l >= WO_F8_FROM) p0_transpose_item_f8<true>(args.in[13] + (size_t)l * DM * DM, DM, DM, DM / 32, (unsigned char*)(ws + WS_WO + l * SZ_WO), 64.f, args.in[6] + l * 2048, args.in[12] + l * 2048, 2048, scr, r, lane);
;                 else p0_transpose_item<0, true>(args.in[13] + (size_t)l * DM * DM, DM, DM, DM / 32, (bf16*)(ws + WS_WO + l * SZ_WO), args.in[6] + l * 2048, args.in[12] + l * 2048, 2048, scr, r, lane); continue; } r -= I_O;
;             if (r < I_UP) { p0_transpose_item_f8<true>(args.in[15] + (size_t)l * DM * FF, DM, FF, FF / 32, (unsigned char*)(ws + WS_WUP + l * SZ_WUP), WUP8_SCALE, args.in[14] + l * DM, args.in[14] + l * DM, DM, scr, r, lane); continue; } r -= I_UP;
;             p0_transpose_item_f8<false>(args.in[16] + (size_t)l * FF * DM, FF, DM, DM / 32, (unsigned char*)(ws + WS_WDN + l * SZ_WDN), 128.f, args.in[16], args.in[16], 0, scr, r, lane);
	s_add_i32 s19, s39, 30
	s_min_u32 s19, s19, 31
	s_lshl_b32 s19, s19, 19
	s_add_u32 s14, s50, s19
	s_addc_u32 s15, s51, 0
	ds_read_b32 v170, v7
	ds_read_b32 v171, v7 offset:512
	ds_read_b32 v172, v7 offset:1024
	ds_read_b32 v173, v7 offset:1536
	ds_read_b32 v174, v7 offset:2048
	ds_read_b32 v175, v7 offset:2560
	ds_read_b32 v176, v7 offset:3072
	ds_read_b32 v177, v7 offset:3584
	ds_read_b32 v196, v7 offset:4096
	ds_read_b32 v197, v7 offset:4608
	ds_read_b32 v198, v7 offset:5120
	ds_read_b32 v199, v7 offset:5632
	ds_read_b32 v200, v7 offset:6144
	ds_read_b32 v201, v7 offset:6656
	ds_read_b32 v202, v7 offset:7168
	ds_read_b32 v203, v7 offset:7680
	s_waitcnt lgkmcnt(0)
	v_max_f32_e32 v170, v170, v170
	v_max_f32_e32 v171, v171, v171
	v_max_f32_e32 v172, v172, v172
	v_max_f32_e32 v173, v173, v173
	v_max_f32_e32 v174, v174, v174
	v_max_f32_e32 v175, v175, v175
	v_max_f32_e32 v176, v176, v176
	v_max_f32_e32 v177, v177, v177
	v_max_f32_e32 v196, v196, v196
	v_max_f32_e32 v197, v197, v197
	v_max_f32_e32 v198, v198, v198
	v_max_f32_e32 v199, v199, v199
	v_max_f32_e32 v200, v200, v200
	v_max_f32_e32 v201, v201, v201
	v_max_f32_e32 v202, v202, v202
	v_max_f32_e32 v203, v203, v203
	v_med3_f32 v170, v170, s20, v13
	v_med3_f32 v171, v171, s20, v13
	v_med3_f32 v172, v172, s20, v13
	v_med3_f32 v173, v173, s20, v13
	v_med3_f32 v174, v174, s20, v13
	v_med3_f32 v175, v175, s20, v13
	v_med3_f32 v176, v176, s20, v13
	v_med3_f32 v177, v177, s20, v13
	v_med3_f32 v196, v196, s20, v13
	v_med3_f32 v197, v197, s20, v13
	v_med3_f32 v198, v198, s20, v13
	v_med3_f32 v199, v199, s20, v13
	v_med3_f32 v200, v200, s20, v13
	v_med3_f32 v201, v201, s20, v13
	v_med3_f32 v202, v202, s20, v13
	v_med3_f32 v203, v203, s20, v13
	v_mov_b32_e32 v208, 0
	v_mov_b32_e32 v209, 0
	v_mov_b32_e32 v210, 0
	v_mov_b32_e32 v211, 0
	v_cvt_pk_fp8_f32 v208, v170, v171
	v_cvt_pk_fp8_f32 v209, v174, v175
	v_cvt_pk_fp8_f32 v210, v196, v197
	v_cvt_pk_fp8_f32 v211, v200, v201
	v_cvt_pk_fp8_f32 v208, v172, v173 op_sel:[0,0,1]
	v_cvt_pk_fp8_f32 v209, v176, v177 op_sel:[0,0,1]
	v_cvt_pk_fp8_f32 v210, v198, v199 op_sel:[0,0,1]
	v_cvt_pk_fp8_f32 v211, v202, v203 op_sel:[0,0,1]
	s_nop 0
	global_store_dwordx4 v28, v[208:211], s[14:15]
	ds_read_b32 v170, v9
	ds_read_b32 v171, v9 offset:512
	ds_read_b32 v172, v9 offset:1024
	ds_read_b32 v173, v9 offset:1536
	ds_read_b32 v174, v9 offset:2048
	ds_read_b32 v175, v9 offset:2560
	ds_read_b32 v176, v9 offset:3072
	ds_read_b32 v177, v9 offset:3584
	ds_read_b32 v196, v9 offset:4096
	ds_read_b32 v197, v9 offset:4608
	ds_read_b32 v198, v9 offset:5120
	ds_read_b32 v199, v9 offset:5632
	ds_read_b32 v200, v9 offset:6144
	ds_read_b32 v201, v9 offset:6656
	ds_read_b32 v202, v9 offset:7168
	ds_read_b32 v203, v9 offset:7680
	s_waitcnt lgkmcnt(0)
	v_max_f32_e32 v170, v170, v170
	v_max_f32_e32 v171, v171, v171
	v_max_f32_e32 v172, v172, v172
	v_max_f32_e32 v173, v173, v173
	v_max_f32_e32 v174, v174, v174
	v_max_f32_e32 v175, v175, v175
	v_max_f32_e32 v176, v176, v176
	v_max_f32_e32 v177, v177, v177
	v_max_f32_e32 v196, v196, v196
	v_max_f32_e32 v197, v197, v197
	v_max_f32_e32 v198, v198, v198
	v_max_f32_e32 v199, v199, v199
	v_max_f32_e32 v200, v200, v200
	v_max_f32_e32 v201, v201, v201
	v_max_f32_e32 v202, v202, v202
	v_max_f32_e32 v203, v203, v203
	v_med3_f32 v170, v170, s20, v13
	v_med3_f32 v171, v171, s20, v13
	v_med3_f32 v172, v172, s20, v13
	v_med3_f32 v173, v173, s20, v13
	v_med3_f32 v174, v174, s20, v13
	v_med3_f32 v175, v175, s20, v13
	v_med3_f32 v176, v176, s20, v13
	v_med3_f32 v177, v177, s20, v13
	v_med3_f32 v196, v196, s20, v13
	v_med3_f32 v197, v197, s20, v13
	v_med3_f32 v198, v198, s20, v13
	v_med3_f32 v199, v199, s20, v13
	v_med3_f32 v200, v200, s20, v13
	v_med3_f32 v201, v201, s20, v13
	v_med3_f32 v202, v202, s20, v13
	v_med3_f32 v203, v203, s20, v13
	v_mov_b32_e32 v208, 0
	v_mov_b32_e32 v209, 0
	v_mov_b32_e32 v210, 0
	v_mov_b32_e32 v211, 0
	v_cvt_pk_fp8_f32 v208, v170, v171
	v_cvt_pk_fp8_f32 v209, v174, v175
	v_cvt_pk_fp8_f32 v210, v196, v197
	v_cvt_pk_fp8_f32 v211, v200, v201
	v_cvt_pk_fp8_f32 v208, v172, v173 op_sel:[0,0,1]
	v_cvt_pk_fp8_f32 v209, v176, v177 op_sel:[0,0,1]
	v_cvt_pk_fp8_f32 v210, v198, v199 op_sel:[0,0,1]
	v_cvt_pk_fp8_f32 v211, v202, v203 op_sel:[0,0,1]
	s_nop 0
	global_store_dwordx4 v29, v[208:211], s[14:15]
	s_waitcnt vmcnt(0) lgkmcnt(0)
	s_barrier
